# v39 with the cache policy of all streamed conversion loads changed from nt to sc0 nt
# speedup vs baseline: 1.0089x; 1.0063x over previous
.LBB0_21:
	s_and_b32 s25, s2, 0x700
	s_ashr_i32 s26, s24, 3
	s_mul_i32 s27, s25, 0xa040
	s_add_u32 s27, s46, s27
	s_addc_u32 s34, s47, 0
	s_lshl_b32 s28, s26, 7
	s_ashr_i32 s29, s28, 31
	s_lshl_b64 s[30:31], s[28:29], 2
	s_add_u32 s27, s27, s30
	s_addc_u32 s30, s34, s31
	s_cmp_gt_i32 s26, 23
	s_cselect_b32 s26, 64, 0
	v_mov_b32_e32 v18, v0
	s_add_u32 s26, s27, s26
	s_addc_u32 s27, s30, 0
	v_lshrrev_b32_e32 v20, 1, v18
	v_lshlrev_b32_e32 v21, 2, v18
	s_lshl_b64 s[28:29], s[28:29], 11
	v_readfirstlane_b32 s33, v18
	v_lshlrev_b32_e32 v22, 4, v18
	v_ashrrev_i32_e32 v84, 4, v18
	v_add_u32_e32 v23, 0x200, v18
	v_add_u32_e32 v24, 0x400, v18
	v_add_u32_e32 v18, 0x600, v18
	v_and_b32_e32 v25, 16, v20
	v_and_b32_e32 v20, 0x7c, v21
	s_add_u32 s28, s0, s28
	v_ashrrev_i32_e32 v86, 4, v23
	v_ashrrev_i32_e32 v90, 4, v18
	v_lshlrev_b32_e32 v18, 2, v20
	v_mul_u32_u24_e32 v23, 0x110, v20
	v_mov_b64_e32 v[20:21], s[26:27]
	s_addc_u32 s27, s1, s29
	s_add_u32 s26, s28, s25
	s_addc_u32 s27, s27, 0
	s_ashr_i32 s25, s33, 1
	s_andn2_b32 s25, s25, 31
	v_ashrrev_i32_e32 v88, 4, v24
	v_or_b32_e32 v24, s25, v25
	s_add_i32 s25, s25, 0
	v_mad_i64_i32 v[20:21], s[28:29], v24, s6, v[20:21]
	v_add3_u32 v101, s25, v25, v23
	v_lshl_add_u64 v[24:25], v[20:21], 0, v[18:19]
	v_add_co_u32_e32 v26, vcc, s7, v24
	s_nop 1
	v_addc_co_u32_e32 v27, vcc, 0, v25, vcc
	v_add_co_u32_e32 v28, vcc, s8, v24
	s_barrier
	s_nop 0
	v_addc_co_u32_e32 v29, vcc, 0, v25, vcc
	v_add_co_u32_e32 v32, vcc, s9, v24
	s_nop 1
	v_addc_co_u32_e32 v33, vcc, 0, v25, vcc
	v_add_co_u32_e32 v36, vcc, s10, v24
	v_and_b32_e32 v18, 0xf0, v22
	s_nop 0
	v_addc_co_u32_e32 v37, vcc, 0, v25, vcc
	v_add_co_u32_e32 v40, vcc, s11, v24
	global_load_dwordx4 v[20:23], v[24:25], off sc0 nt
	s_nop 0
	v_addc_co_u32_e32 v41, vcc, 0, v25, vcc
	v_add_co_u32_e32 v44, vcc, s12, v24
	v_add_u32_e32 v100, 0, v18
	s_nop 0
	v_addc_co_u32_e32 v45, vcc, 0, v25, vcc
	v_add_co_u32_e32 v48, vcc, s13, v24
	v_lshl_add_u64 v[102:103], s[26:27], 0, v[18:19]
	s_nop 0
	v_addc_co_u32_e32 v49, vcc, 0, v25, vcc
	v_add_co_u32_e32 v52, vcc, s14, v24
	v_mov_b32_e32 v2, v19
	s_nop 0
	v_addc_co_u32_e32 v53, vcc, 0, v25, vcc
	v_add_co_u32_e32 v56, vcc, s15, v24
	v_mov_b32_e32 v3, v19
	s_nop 0
	v_addc_co_u32_e32 v57, vcc, 0, v25, vcc
	v_add_co_u32_e32 v60, vcc, s16, v24
	v_mov_b32_e32 v4, v19
	s_nop 0
	v_addc_co_u32_e32 v61, vcc, 0, v25, vcc
	v_add_co_u32_e32 v64, vcc, s17, v24
	v_mov_b32_e32 v5, v19
	s_nop 0
	v_addc_co_u32_e32 v65, vcc, 0, v25, vcc
	v_add_co_u32_e32 v68, vcc, s18, v24
	v_mov_b32_e32 v6, v19
	s_nop 0
	v_addc_co_u32_e32 v69, vcc, 0, v25, vcc
	v_add_co_u32_e32 v72, vcc, s19, v24
	v_mov_b32_e32 v7, v19
	s_nop 0
	v_addc_co_u32_e32 v73, vcc, 0, v25, vcc
	v_add_co_u32_e32 v76, vcc, s20, v24
	v_mov_b32_e32 v8, v19
	s_nop 0
	v_addc_co_u32_e32 v77, vcc, 0, v25, vcc
	v_add_co_u32_e32 v80, vcc, s21, v24
	v_mov_b32_e32 v9, v19
	s_nop 0
	v_addc_co_u32_e32 v81, vcc, 0, v25, vcc
	global_load_dwordx4 v[24:27], v[26:27], off offset:64 sc0 nt
	s_nop 0
	global_load_dwordx4 v[28:31], v[28:29], off offset:128 sc0 nt
	s_nop 0
	global_load_dwordx4 v[32:35], v[32:33], off offset:192 sc0 nt
	s_nop 0
	global_load_dwordx4 v[36:39], v[36:37], off offset:256 sc0 nt
	s_nop 0
	global_load_dwordx4 v[40:43], v[40:41], off offset:320 sc0 nt
	s_nop 0
	global_load_dwordx4 v[44:47], v[44:45], off offset:384 sc0 nt
	s_nop 0
	global_load_dwordx4 v[48:51], v[48:49], off offset:448 sc0 nt
	s_nop 0
	global_load_dwordx4 v[52:55], v[52:53], off offset:512 sc0 nt
	s_nop 0
	global_load_dwordx4 v[56:59], v[56:57], off offset:576 sc0 nt
	s_nop 0
	global_load_dwordx4 v[60:63], v[60:61], off offset:640 sc0 nt
	s_nop 0
	global_load_dwordx4 v[64:67], v[64:65], off offset:704 sc0 nt
	s_nop 0
	global_load_dwordx4 v[68:71], v[68:69], off offset:768 sc0 nt
	s_nop 0
	global_load_dwordx4 v[72:75], v[72:73], off offset:832 sc0 nt
	s_nop 0
	global_load_dwordx4 v[76:79], v[76:77], off offset:896 sc0 nt
	s_nop 0
	global_load_dwordx4 v[80:83], v[80:81], off offset:960 sc0 nt
	v_mov_b32_e32 v10, v19
	v_mov_b32_e32 v11, v19
	v_mov_b32_e32 v12, v19
	v_mov_b32_e32 v13, v19
	v_mov_b32_e32 v14, v19
	v_mov_b32_e32 v15, v19
	v_mov_b32_e32 v16, v19
	v_mov_b32_e32 v17, v19
	v_ashrrev_i32_e32 v85, 31, v84
	v_ashrrev_i32_e32 v87, 31, v86
	v_ashrrev_i32_e32 v89, 31, v88
	v_ashrrev_i32_e32 v91, 31, v90
	v_lshlrev_b64 v[92:93], 11, v[84:85]
	v_mad_u64_u32 v[84:85], s[26:27], v84, s23, v[100:101]
	v_lshlrev_b64 v[94:95], 11, v[86:87]
	v_lshlrev_b64 v[96:97], 11, v[88:89]
	v_lshlrev_b64 v[98:99], 11, v[90:91]
	v_mad_u64_u32 v[86:87], s[26:27], v86, s23, v[100:101]
	v_mad_u64_u32 v[88:89], s[26:27], v88, s23, v[100:101]
	v_mad_u64_u32 v[90:91], s[26:27], v90, s23, v[100:101]
	s_add_i32 s24, s24, s80
	s_add_i32 s2, s2, s3
	s_waitcnt vmcnt(15)
	v_mul_f32_e32 v18, 0x43800000, v20
	v_mul_f32_e32 v20, 0x43800000, v21
	v_mul_f32_e32 v21, 0x43800000, v22
	v_mul_f32_e32 v22, 0x43800000, v23
	v_med3_f32 v18, v18, s22, v1
	v_med3_f32 v20, v20, s22, v1
	v_med3_f32 v21, v21, s22, v1
	v_med3_f32 v22, v22, s22, v1
	s_cmpk_lt_i32 s24, 0x280
	v_lshl_add_u64 v[92:93], v[102:103], 0, v[92:93]
	v_lshl_add_u64 v[94:95], v[102:103], 0, v[94:95]
	v_lshl_add_u64 v[96:97], v[102:103], 0, v[96:97]
	v_lshl_add_u64 v[98:99], v[102:103], 0, v[98:99]
	s_waitcnt vmcnt(14)
	v_mul_f32_e32 v23, 0x43800000, v24
	s_waitcnt vmcnt(13)
	v_mul_f32_e32 v24, 0x43800000, v28
	s_waitcnt vmcnt(12)
	v_mul_f32_e32 v28, 0x43800000, v32
	s_waitcnt vmcnt(11)
	v_mul_f32_e32 v32, 0x43800000, v36
	s_waitcnt vmcnt(10)
	v_mul_f32_e32 v36, 0x43800000, v40
	s_waitcnt vmcnt(9)
	v_mul_f32_e32 v40, 0x43800000, v44
	s_waitcnt vmcnt(8)
	v_mul_f32_e32 v44, 0x43800000, v48
	s_waitcnt vmcnt(7)
	v_mul_f32_e32 v48, 0x43800000, v52
	s_waitcnt vmcnt(6)
	v_mul_f32_e32 v52, 0x43800000, v56
	s_waitcnt vmcnt(5)
	v_mul_f32_e32 v56, 0x43800000, v60
	s_waitcnt vmcnt(4)
	v_mul_f32_e32 v60, 0x43800000, v64
	s_waitcnt vmcnt(3)
	v_mul_f32_e32 v64, 0x43800000, v68
	s_waitcnt vmcnt(2)
	v_mul_f32_e32 v68, 0x43800000, v72
	v_mul_f32_e32 v25, 0x43800000, v25
	v_mul_f32_e32 v37, 0x43800000, v37
	v_mul_f32_e32 v41, 0x43800000, v41
	v_mul_f32_e32 v53, 0x43800000, v53
	v_mul_f32_e32 v57, 0x43800000, v57
	v_mul_f32_e32 v69, 0x43800000, v69
	v_mul_f32_e32 v73, 0x43800000, v73
	v_med3_f32 v23, v23, s22, v1
	v_med3_f32 v32, v32, s22, v1
	v_med3_f32 v36, v36, s22, v1
	v_med3_f32 v48, v48, s22, v1
	v_med3_f32 v52, v52, s22, v1
	v_med3_f32 v64, v64, s22, v1
	v_med3_f32 v68, v68, s22, v1
	v_mul_f32_e32 v26, 0x43800000, v26
	v_mul_f32_e32 v38, 0x43800000, v38
	v_mul_f32_e32 v42, 0x43800000, v42
	v_mul_f32_e32 v54, 0x43800000, v54
	v_mul_f32_e32 v58, 0x43800000, v58
	v_mul_f32_e32 v70, 0x43800000, v70
	v_mul_f32_e32 v74, 0x43800000, v74
	v_med3_f32 v25, v25, s22, v1
	v_med3_f32 v37, v37, s22, v1
	v_med3_f32 v41, v41, s22, v1
	v_med3_f32 v53, v53, s22, v1
	v_med3_f32 v57, v57, s22, v1
	v_med3_f32 v69, v69, s22, v1
	v_med3_f32 v73, v73, s22, v1
	v_cvt_pk_fp8_f32 v2, v18, v23
	v_cvt_pk_fp8_f32 v3, v32, v36
	v_cvt_pk_fp8_f32 v4, v48, v52
	v_cvt_pk_fp8_f32 v5, v64, v68
	v_mul_f32_e32 v27, 0x43800000, v27
	v_mul_f32_e32 v39, 0x43800000, v39
	v_mul_f32_e32 v43, 0x43800000, v43
	v_mul_f32_e32 v55, 0x43800000, v55
	v_mul_f32_e32 v59, 0x43800000, v59
	v_mul_f32_e32 v71, 0x43800000, v71
	v_mul_f32_e32 v75, 0x43800000, v75
	v_med3_f32 v26, v26, s22, v1
	v_med3_f32 v38, v38, s22, v1
	v_med3_f32 v42, v42, s22, v1
	v_med3_f32 v54, v54, s22, v1
	v_med3_f32 v58, v58, s22, v1
	v_med3_f32 v70, v70, s22, v1
	v_med3_f32 v74, v74, s22, v1
	v_cvt_pk_fp8_f32 v6, v20, v25
	v_cvt_pk_fp8_f32 v7, v37, v41
	v_cvt_pk_fp8_f32 v8, v53, v57
	v_cvt_pk_fp8_f32 v9, v69, v73
	s_waitcnt vmcnt(1)
	v_mul_f32_e32 v72, 0x43800000, v76
	s_waitcnt vmcnt(0)
	v_mul_f32_e32 v76, 0x43800000, v80
	v_med3_f32 v27, v27, s22, v1
	v_med3_f32 v39, v39, s22, v1
	v_med3_f32 v43, v43, s22, v1
	v_med3_f32 v55, v55, s22, v1
	v_med3_f32 v59, v59, s22, v1
	v_med3_f32 v71, v71, s22, v1
	v_med3_f32 v75, v75, s22, v1
	v_cvt_pk_fp8_f32 v10, v21, v26
	v_cvt_pk_fp8_f32 v11, v38, v42
	v_cvt_pk_fp8_f32 v12, v54, v58
	v_cvt_pk_fp8_f32 v13, v70, v74
	v_mul_f32_e32 v29, 0x43800000, v29
	v_mul_f32_e32 v33, 0x43800000, v33
	v_mul_f32_e32 v45, 0x43800000, v45
	v_mul_f32_e32 v49, 0x43800000, v49
	v_mul_f32_e32 v61, 0x43800000, v61
	v_mul_f32_e32 v65, 0x43800000, v65
	v_mul_f32_e32 v77, 0x43800000, v77
	v_mul_f32_e32 v80, 0x43800000, v81
	v_med3_f32 v24, v24, s22, v1
	v_med3_f32 v28, v28, s22, v1
	v_med3_f32 v40, v40, s22, v1
	v_med3_f32 v44, v44, s22, v1
	v_med3_f32 v56, v56, s22, v1
	v_med3_f32 v60, v60, s22, v1
	v_med3_f32 v72, v72, s22, v1
	v_med3_f32 v76, v76, s22, v1
	v_cvt_pk_fp8_f32 v14, v22, v27
	v_cvt_pk_fp8_f32 v15, v39, v43
	v_cvt_pk_fp8_f32 v16, v55, v59
	v_cvt_pk_fp8_f32 v17, v71, v75
	v_mul_f32_e32 v30, 0x43800000, v30
	v_mul_f32_e32 v34, 0x43800000, v34
	v_mul_f32_e32 v46, 0x43800000, v46
	v_mul_f32_e32 v50, 0x43800000, v50
	v_mul_f32_e32 v62, 0x43800000, v62
	v_mul_f32_e32 v66, 0x43800000, v66
	v_mul_f32_e32 v78, 0x43800000, v78
	v_mul_f32_e32 v81, 0x43800000, v82
	v_med3_f32 v29, v29, s22, v1
	v_med3_f32 v33, v33, s22, v1
	v_med3_f32 v45, v45, s22, v1
	v_med3_f32 v49, v49, s22, v1
	v_med3_f32 v61, v61, s22, v1
	v_med3_f32 v65, v65, s22, v1
	v_med3_f32 v77, v77, s22, v1
	v_med3_f32 v80, v80, s22, v1
	v_cvt_pk_fp8_f32 v2, v24, v28 op_sel:[0,0,1]
	v_cvt_pk_fp8_f32 v3, v40, v44 op_sel:[0,0,1]
	v_cvt_pk_fp8_f32 v4, v56, v60 op_sel:[0,0,1]
	v_cvt_pk_fp8_f32 v5, v72, v76 op_sel:[0,0,1]
	v_mul_f32_e32 v31, 0x43800000, v31
	v_mul_f32_e32 v35, 0x43800000, v35
	v_mul_f32_e32 v47, 0x43800000, v47
	v_mul_f32_e32 v51, 0x43800000, v51
	v_mul_f32_e32 v63, 0x43800000, v63
	v_mul_f32_e32 v67, 0x43800000, v67
	v_mul_f32_e32 v79, 0x43800000, v79
	v_mul_f32_e32 v82, 0x43800000, v83
	v_med3_f32 v30, v30, s22, v1
	v_med3_f32 v34, v34, s22, v1
	v_med3_f32 v46, v46, s22, v1
	v_med3_f32 v50, v50, s22, v1
	v_med3_f32 v62, v62, s22, v1
	v_med3_f32 v66, v66, s22, v1
	v_med3_f32 v78, v78, s22, v1
	v_med3_f32 v81, v81, s22, v1
	v_cvt_pk_fp8_f32 v6, v29, v33 op_sel:[0,0,1]
	v_cvt_pk_fp8_f32 v7, v45, v49 op_sel:[0,0,1]
	v_cvt_pk_fp8_f32 v8, v61, v65 op_sel:[0,0,1]
	v_cvt_pk_fp8_f32 v9, v77, v80 op_sel:[0,0,1]
	v_med3_f32 v31, v31, s22, v1
	v_med3_f32 v35, v35, s22, v1
	v_med3_f32 v47, v47, s22, v1
	v_med3_f32 v51, v51, s22, v1
	v_med3_f32 v63, v63, s22, v1
	v_med3_f32 v67, v67, s22, v1
	v_med3_f32 v79, v79, s22, v1
	v_med3_f32 v82, v82, s22, v1
	v_cvt_pk_fp8_f32 v10, v30, v34 op_sel:[0,0,1]
	v_cvt_pk_fp8_f32 v11, v46, v50 op_sel:[0,0,1]
	v_cvt_pk_fp8_f32 v12, v62, v66 op_sel:[0,0,1]
	v_cvt_pk_fp8_f32 v13, v78, v81 op_sel:[0,0,1]
	v_cvt_pk_fp8_f32 v14, v31, v35 op_sel:[0,0,1]
	v_cvt_pk_fp8_f32 v15, v47, v51 op_sel:[0,0,1]
	v_cvt_pk_fp8_f32 v16, v63, v67 op_sel:[0,0,1]
	v_cvt_pk_fp8_f32 v17, v79, v82 op_sel:[0,0,1]
	ds_write_b128 v101, v[2:5]
	ds_write_b128 v101, v[6:9] offset:272
	ds_write_b128 v101, v[10:13] offset:544
	ds_write_b128 v101, v[14:17] offset:816
	s_waitcnt lgkmcnt(0)
	s_barrier
	ds_read_b128 v[2:5], v84
	ds_read_b128 v[6:9], v86
	ds_read_b128 v[10:13], v88
	ds_read_b128 v[14:17], v90
	s_waitcnt lgkmcnt(3)
	global_store_dwordx4 v[92:93], v[2:5], off
	s_waitcnt lgkmcnt(2)
	global_store_dwordx4 v[94:95], v[6:9], off
	s_waitcnt lgkmcnt(1)
	global_store_dwordx4 v[96:97], v[10:13], off
	s_waitcnt lgkmcnt(0)
	global_store_dwordx4 v[98:99], v[14:17], off
	s_barrier
	s_cbranch_scc1 .LBB0_21

.LBB0_26:
	s_add_i32 s6, s2, 0x80
	s_cmpk_gt_i32 s6, 0x7f
	s_mov_b64 s[6:7], -1
	s_cbranch_scc0 .LBB0_28
	v_readlane_b32 s36, v254, 30
	s_cmp_lt_u32 s2, 64
	v_readlane_b32 s42, v254, 36
	v_readlane_b32 s43, v254, 37
	v_readlane_b32 s44, v254, 38
	v_readlane_b32 s45, v254, 39
	s_cselect_b32 s6, s13, 0x3400000
	s_cselect_b32 s7, s43, s45
	s_cselect_b32 s33, s42, s44
	s_add_i32 s34, s10, 0xffff7f00
	s_and_b32 s34, s34, 0x300
	s_lshl_b32 s35, s34, 13
	s_add_u32 s33, s33, s35
	v_readlane_b32 s50, v254, 44
	s_addc_u32 s7, s7, 0
	s_and_b32 s35, s3, 0x780
	s_lshl_b32 s50, s35, 2
	v_readlane_b32 s51, v254, 45
	s_add_u32 s50, s33, s50
	s_addc_u32 s51, s7, 0
	s_add_u32 s6, s78, s6
	s_addc_u32 s7, s79, 0
	s_lshl_b32 s33, s35, 10
	s_add_u32 s6, s6, s33
	v_mov_b32_e32 v80, v0
	s_addc_u32 s7, s7, 0
	s_add_u32 s6, s6, s34
	v_readfirstlane_b32 s31, v80
	s_addc_u32 s7, s7, 0
	s_ashr_i32 s31, s31, 1
	v_lshrrev_b32_e32 v2, 1, v80
	s_andn2_b32 s31, s31, 31
	v_and_b32_e32 v72, 16, v2
	v_or_b32_e32 v2, s31, v72
	v_ashrrev_i32_e32 v3, 31, v2
	v_lshlrev_b32_e32 v4, 2, v80
	v_lshlrev_b64 v[2:3], 13, v[2:3]
	v_and_b32_e32 v73, 0x7c, v4
	v_lshl_add_u64 v[2:3], s[50:51], 0, v[2:3]
	v_lshlrev_b32_e32 v62, 2, v73
	v_lshl_add_u64 v[58:59], v[2:3], 0, v[62:63]
	v_add_co_u32_e32 v6, vcc, s14, v58
	s_nop 1
	v_addc_co_u32_e32 v7, vcc, 0, v59, vcc
	v_add_co_u32_e32 v10, vcc, s15, v58
	s_barrier
	s_nop 0
	v_addc_co_u32_e32 v11, vcc, 0, v59, vcc
	v_add_co_u32_e32 v12, vcc, s16, v58
	s_nop 1
	v_addc_co_u32_e32 v13, vcc, 0, v59, vcc
	v_add_co_u32_e32 v14, vcc, s17, v58
	global_load_dwordx4 v[2:5], v[58:59], off sc0 nt
	s_nop 0
	global_load_dwordx4 v[6:9], v[6:7], off sc0 nt
	v_addc_co_u32_e32 v15, vcc, 0, v59, vcc
	v_add_co_u32_e32 v22, vcc, s18, v58
	global_load_dwordx4 v[18:21], v[10:11], off sc0 nt
	s_nop 0
	global_load_dwordx4 v[10:13], v[12:13], off sc0 nt
	v_addc_co_u32_e32 v23, vcc, 0, v59, vcc
	v_add_co_u32_e32 v26, vcc, s19, v58
	global_load_dwordx4 v[14:17], v[14:15], off sc0 nt
	s_nop 0
	global_load_dwordx4 v[22:25], v[22:23], off sc0 nt
	v_addc_co_u32_e32 v27, vcc, 0, v59, vcc
	v_add_co_u32_e32 v28, vcc, s20, v58
	v_mov_b32_e32 v68, v63
	s_nop 0
	v_addc_co_u32_e32 v29, vcc, 0, v59, vcc
	v_add_co_u32_e32 v30, vcc, s21, v58
	global_load_dwordx4 v[34:37], v[26:27], off sc0 nt
	s_nop 0
	global_load_dwordx4 v[26:29], v[28:29], off sc0 nt
	v_addc_co_u32_e32 v31, vcc, 0, v59, vcc
	v_add_co_u32_e32 v38, vcc, s22, v58
	v_mov_b32_e32 v69, v63
	s_nop 0
	v_addc_co_u32_e32 v39, vcc, 0, v59, vcc
	v_add_co_u32_e32 v42, vcc, s23, v58
	global_load_dwordx4 v[30:33], v[30:31], off sc0 nt
	s_nop 0
	global_load_dwordx4 v[38:41], v[38:39], off sc0 nt
	v_addc_co_u32_e32 v43, vcc, 0, v59, vcc
	v_add_co_u32_e32 v44, vcc, s24, v58
	v_mov_b32_e32 v70, v63
	s_nop 0
	v_addc_co_u32_e32 v45, vcc, 0, v59, vcc
	v_add_co_u32_e32 v46, vcc, s25, v58
	global_load_dwordx4 v[50:53], v[42:43], off sc0 nt
	s_nop 0
	global_load_dwordx4 v[42:45], v[44:45], off sc0 nt
	v_addc_co_u32_e32 v47, vcc, 0, v59, vcc
	v_add_co_u32_e32 v54, vcc, s26, v58
	v_mov_b32_e32 v71, v63
	s_nop 0
	v_addc_co_u32_e32 v55, vcc, 0, v59, vcc
	global_load_dwordx4 v[46:49], v[46:47], off sc0 nt
	s_nop 0
	global_load_dwordx4 v[54:57], v[54:55], off sc0 nt
	v_add_co_u32_e32 v60, vcc, s27, v58
	s_add_i32 s31, s31, 0
	s_nop 0
	v_addc_co_u32_e32 v61, vcc, 0, v59, vcc
	v_add_co_u32_e32 v58, vcc, s28, v58
	global_load_dwordx4 v[64:67], v[60:61], off sc0 nt
	s_nop 0
	v_addc_co_u32_e32 v59, vcc, 0, v59, vcc
	global_load_dwordx4 v[58:61], v[58:59], off sc0 nt
	v_mov_b32_e32 v74, v63
	v_mov_b32_e32 v75, v63
	v_mov_b32_e32 v76, v63
	v_mov_b32_e32 v77, v63
	v_mov_b32_e32 v78, v63
	v_mov_b32_e32 v79, v63
	v_readlane_b32 s37, v254, 31
	v_readlane_b32 s38, v254, 32
	v_readlane_b32 s39, v254, 33
	v_readlane_b32 s40, v254, 34
	v_readlane_b32 s41, v254, 35
	v_readlane_b32 s46, v254, 40
	v_readlane_b32 s47, v254, 41
	v_readlane_b32 s48, v254, 42
	v_readlane_b32 s49, v254, 43
	s_waitcnt vmcnt(15)
	v_mul_f32_e32 v2, 0x43800000, v2
	s_waitcnt vmcnt(14)
	v_mul_f32_e32 v6, 0x43800000, v6
	v_med3_f32 v2, v2, s29, v1
	v_med3_f32 v6, v6, s29, v1
	v_cvt_pk_fp8_f32 v68, v2, v6
	s_waitcnt vmcnt(13)
	v_mul_f32_e32 v18, 0x43800000, v18
	s_waitcnt vmcnt(12)
	v_mul_f32_e32 v2, 0x43800000, v10
	v_med3_f32 v6, v18, s29, v1
	v_med3_f32 v2, v2, s29, v1
	v_cvt_pk_fp8_f32 v68, v6, v2 op_sel:[0,0,1]
	s_waitcnt vmcnt(11)
	v_mul_f32_e32 v2, 0x43800000, v14
	s_waitcnt vmcnt(10)
	v_mul_f32_e32 v6, 0x43800000, v22
	v_med3_f32 v2, v2, s29, v1
	v_med3_f32 v6, v6, s29, v1
	v_cvt_pk_fp8_f32 v69, v2, v6
	s_waitcnt vmcnt(9)
	v_mul_f32_e32 v10, 0x43800000, v34
	s_waitcnt vmcnt(8)
	v_mul_f32_e32 v2, 0x43800000, v26
	v_med3_f32 v6, v10, s29, v1
	v_med3_f32 v2, v2, s29, v1
	v_cvt_pk_fp8_f32 v69, v6, v2 op_sel:[0,0,1]
	s_waitcnt vmcnt(7)
	v_mul_f32_e32 v2, 0x43800000, v30
	s_waitcnt vmcnt(6)
	v_mul_f32_e32 v6, 0x43800000, v38
	v_med3_f32 v2, v2, s29, v1
	v_med3_f32 v6, v6, s29, v1
	v_cvt_pk_fp8_f32 v70, v2, v6
	s_waitcnt vmcnt(5)
	v_mul_f32_e32 v10, 0x43800000, v50
	s_waitcnt vmcnt(4)
	v_mul_f32_e32 v2, 0x43800000, v42
	v_med3_f32 v6, v10, s29, v1
	v_med3_f32 v2, v2, s29, v1
	v_cvt_pk_fp8_f32 v70, v6, v2 op_sel:[0,0,1]
	s_waitcnt vmcnt(3)
	v_mul_f32_e32 v2, 0x43800000, v46
	s_waitcnt vmcnt(2)
	v_mul_f32_e32 v6, 0x43800000, v54
	v_med3_f32 v2, v2, s29, v1
	v_med3_f32 v6, v6, s29, v1
	v_cvt_pk_fp8_f32 v71, v2, v6
	s_waitcnt vmcnt(1)
	v_mul_f32_e32 v10, 0x43800000, v64
	v_med3_f32 v6, v10, s29, v1
	s_waitcnt vmcnt(0)
	v_mul_f32_e32 v2, 0x43800000, v58
	v_med3_f32 v2, v2, s29, v1
	v_cvt_pk_fp8_f32 v71, v6, v2 op_sel:[0,0,1]
	v_mul_u32_u24_e32 v2, 0x110, v73
	v_add3_u32 v6, s31, v72, v2
	v_mul_f32_e32 v2, 0x43800000, v3
	v_mul_f32_e32 v3, 0x43800000, v7
	v_med3_f32 v2, v2, s29, v1
	v_med3_f32 v3, v3, s29, v1
	v_mov_b32_e32 v72, v63
	v_cvt_pk_fp8_f32 v72, v2, v3
	v_mul_f32_e32 v7, 0x43800000, v19
	v_mul_f32_e32 v2, 0x43800000, v11
	v_med3_f32 v3, v7, s29, v1
	v_med3_f32 v2, v2, s29, v1
	v_cvt_pk_fp8_f32 v72, v3, v2 op_sel:[0,0,1]
	v_mul_f32_e32 v2, 0x43800000, v15
	v_mul_f32_e32 v3, 0x43800000, v23
	v_med3_f32 v2, v2, s29, v1
	v_med3_f32 v3, v3, s29, v1
	v_mov_b32_e32 v73, v63
	v_cvt_pk_fp8_f32 v73, v2, v3
	v_mul_f32_e32 v7, 0x43800000, v35
	v_mul_f32_e32 v2, 0x43800000, v27
	v_med3_f32 v3, v7, s29, v1
	v_med3_f32 v2, v2, s29, v1
	v_cvt_pk_fp8_f32 v73, v3, v2 op_sel:[0,0,1]
	v_mul_f32_e32 v2, 0x43800000, v31
	v_mul_f32_e32 v3, 0x43800000, v39
	v_med3_f32 v2, v2, s29, v1
	v_med3_f32 v3, v3, s29, v1
	v_cvt_pk_fp8_f32 v74, v2, v3
	v_mul_f32_e32 v7, 0x43800000, v51
	v_mul_f32_e32 v2, 0x43800000, v43
	v_med3_f32 v3, v7, s29, v1
	v_med3_f32 v2, v2, s29, v1
	v_cvt_pk_fp8_f32 v74, v3, v2 op_sel:[0,0,1]
	v_mul_f32_e32 v2, 0x43800000, v47
	v_mul_f32_e32 v3, 0x43800000, v55
	v_med3_f32 v2, v2, s29, v1
	v_med3_f32 v3, v3, s29, v1
	v_cvt_pk_fp8_f32 v75, v2, v3
	v_mul_f32_e32 v7, 0x43800000, v65
	v_mul_f32_e32 v2, 0x43800000, v59
	v_med3_f32 v3, v7, s29, v1
	v_med3_f32 v2, v2, s29, v1
	v_cvt_pk_fp8_f32 v75, v3, v2 op_sel:[0,0,1]
	v_mul_f32_e32 v2, 0x43800000, v4
	v_mul_f32_e32 v3, 0x43800000, v8
	v_med3_f32 v2, v2, s29, v1
	v_med3_f32 v3, v3, s29, v1
	v_cvt_pk_fp8_f32 v76, v2, v3
	v_mul_f32_e32 v4, 0x43800000, v20
	v_mul_f32_e32 v2, 0x43800000, v12
	v_med3_f32 v3, v4, s29, v1
	v_med3_f32 v2, v2, s29, v1
	v_cvt_pk_fp8_f32 v76, v3, v2 op_sel:[0,0,1]
	v_mul_f32_e32 v2, 0x43800000, v16
	v_mul_f32_e32 v3, 0x43800000, v24
	v_med3_f32 v2, v2, s29, v1
	v_med3_f32 v3, v3, s29, v1
	v_cvt_pk_fp8_f32 v77, v2, v3
	v_mul_f32_e32 v4, 0x43800000, v36
	v_mul_f32_e32 v2, 0x43800000, v28
	v_med3_f32 v3, v4, s29, v1
	v_med3_f32 v2, v2, s29, v1
	v_cvt_pk_fp8_f32 v77, v3, v2 op_sel:[0,0,1]
	v_mul_f32_e32 v2, 0x43800000, v32
	v_mul_f32_e32 v3, 0x43800000, v40
	v_med3_f32 v2, v2, s29, v1
	v_med3_f32 v3, v3, s29, v1
	v_cvt_pk_fp8_f32 v78, v2, v3
	v_mul_f32_e32 v4, 0x43800000, v52
	v_mul_f32_e32 v2, 0x43800000, v44
	v_med3_f32 v3, v4, s29, v1
	v_med3_f32 v2, v2, s29, v1
	v_cvt_pk_fp8_f32 v78, v3, v2 op_sel:[0,0,1]
	v_mul_f32_e32 v2, 0x43800000, v48
	v_mul_f32_e32 v3, 0x43800000, v56
	v_med3_f32 v2, v2, s29, v1
	v_med3_f32 v3, v3, s29, v1
	v_cvt_pk_fp8_f32 v79, v2, v3
	v_mul_f32_e32 v4, 0x43800000, v66
	v_mul_f32_e32 v2, 0x43800000, v60
	v_med3_f32 v3, v4, s29, v1
	v_med3_f32 v2, v2, s29, v1
	v_cvt_pk_fp8_f32 v79, v3, v2 op_sel:[0,0,1]
	v_mul_f32_e32 v2, 0x43800000, v5
	v_mul_f32_e32 v3, 0x43800000, v9
	v_med3_f32 v5, v2, s29, v1
	v_med3_f32 v3, v3, s29, v1
	v_mov_b32_e32 v2, v63
	v_cvt_pk_fp8_f32 v2, v5, v3
	v_mul_f32_e32 v4, 0x43800000, v21
	v_mul_f32_e32 v3, 0x43800000, v13
	v_med3_f32 v4, v4, s29, v1
	v_med3_f32 v3, v3, s29, v1
	v_cvt_pk_fp8_f32 v2, v4, v3 op_sel:[0,0,1]
	v_mul_f32_e32 v3, 0x43800000, v17
	v_mul_f32_e32 v4, 0x43800000, v25
	v_med3_f32 v7, v3, s29, v1
	v_med3_f32 v4, v4, s29, v1
	v_mov_b32_e32 v3, v63
	v_cvt_pk_fp8_f32 v3, v7, v4
	v_mul_f32_e32 v5, 0x43800000, v37
	v_mul_f32_e32 v4, 0x43800000, v29
	v_med3_f32 v5, v5, s29, v1
	v_med3_f32 v4, v4, s29, v1
	v_cvt_pk_fp8_f32 v3, v5, v4 op_sel:[0,0,1]
	v_mul_f32_e32 v4, 0x43800000, v33
	v_mul_f32_e32 v5, 0x43800000, v41
	v_med3_f32 v8, v4, s29, v1
	v_med3_f32 v5, v5, s29, v1
	v_mov_b32_e32 v4, v63
	v_cvt_pk_fp8_f32 v4, v8, v5
	v_mul_f32_e32 v7, 0x43800000, v53
	v_mul_f32_e32 v5, 0x43800000, v45
	v_med3_f32 v7, v7, s29, v1
	v_med3_f32 v5, v5, s29, v1
	v_cvt_pk_fp8_f32 v4, v7, v5 op_sel:[0,0,1]
	v_mul_f32_e32 v5, 0x43800000, v49
	v_mul_f32_e32 v7, 0x43800000, v57
	v_med3_f32 v9, v5, s29, v1
	v_med3_f32 v7, v7, s29, v1
	v_mov_b32_e32 v5, v63
	v_cvt_pk_fp8_f32 v5, v9, v7
	v_mul_f32_e32 v8, 0x43800000, v67
	v_mul_f32_e32 v7, 0x43800000, v61
	v_med3_f32 v8, v8, s29, v1
	v_med3_f32 v7, v7, s29, v1
	v_cvt_pk_fp8_f32 v5, v8, v7 op_sel:[0,0,1]
	ds_write_b128 v6, v[68:71]
	ds_write_b128 v6, v[72:75] offset:272
	ds_write_b128 v6, v[76:79] offset:544
	ds_write_b128 v6, v[2:5] offset:816
	v_lshlrev_b32_e32 v2, 4, v80
	v_ashrrev_i32_e32 v6, 4, v80
	v_and_b32_e32 v62, 0xf0, v2
	v_ashrrev_i32_e32 v7, 31, v6
	v_lshl_add_u64 v[10:11], s[6:7], 0, v[62:63]
	v_mul_lo_u32 v2, v6, s30
	v_lshlrev_b64 v[6:7], 10, v[6:7]
	v_lshl_add_u64 v[12:13], v[10:11], 0, v[6:7]
	v_add_u32_e32 v6, 0x200, v80
	v_add3_u32 v2, 0, v2, v62
	v_ashrrev_i32_e32 v14, 4, v6
	s_waitcnt lgkmcnt(0)
	s_barrier
	ds_read_b128 v[2:5], v2
	v_mul_lo_u32 v6, v14, s30
	v_add3_u32 v6, 0, v6, v62
	ds_read_b128 v[6:9], v6
	v_ashrrev_i32_e32 v15, 31, v14
	s_waitcnt lgkmcnt(1)
	global_store_dwordx4 v[12:13], v[2:5], off
	s_mov_b64 s[6:7], 0
	s_nop 0
	v_lshlrev_b64 v[2:3], 10, v[14:15]
	v_lshl_add_u64 v[2:3], v[10:11], 0, v[2:3]
	s_waitcnt lgkmcnt(0)
	global_store_dwordx4 v[2:3], v[6:9], off
	v_add_u32_e32 v2, 0x400, v80
	s_nop 0
	v_ashrrev_i32_e32 v6, 4, v2
	v_ashrrev_i32_e32 v7, 31, v6
	v_mul_lo_u32 v2, v6, s30
	v_lshlrev_b64 v[6:7], 10, v[6:7]
	v_lshl_add_u64 v[12:13], v[10:11], 0, v[6:7]
	v_add_u32_e32 v6, 0x600, v80
	v_add3_u32 v2, 0, v2, v62
	v_ashrrev_i32_e32 v14, 4, v6
	ds_read_b128 v[2:5], v2
	v_mul_lo_u32 v6, v14, s30
	v_add3_u32 v6, 0, v6, v62
	ds_read_b128 v[6:9], v6
	v_ashrrev_i32_e32 v15, 31, v14
	s_waitcnt lgkmcnt(1)
	global_store_dwordx4 v[12:13], v[2:5], off
	s_nop 1
	v_lshlrev_b64 v[2:3], 10, v[14:15]
	v_lshl_add_u64 v[2:3], v[10:11], 0, v[2:3]
	s_waitcnt lgkmcnt(0)
	global_store_dwordx4 v[2:3], v[6:9], off
	s_barrier
.LBB0_28:
	s_andn2_b64 vcc, exec, s[6:7]
	s_cbranch_vccnz .LBB0_25
	s_add_i32 s6, s10, 0xffffff00
	s_and_b32 s33, s6, 0x700
	v_readlane_b32 s36, v254, 30
	s_lshl_b32 s6, s33, 13
	v_readlane_b32 s46, v254, 40
	v_readlane_b32 s47, v254, 41
	s_add_u32 s34, s46, s6
	s_addc_u32 s35, s47, 0
	s_and_b32 s6, s11, 0xffffff80
	v_readlane_b32 s50, v254, 44
	v_readlane_b32 s51, v254, 45
	s_ashr_i32 s7, s6, 31
	s_lshl_b64 s[50:51], s[6:7], 2
	s_add_u32 s50, s34, s50
	s_addc_u32 s51, s35, s51
	s_lshl_b64 s[6:7], s[6:7], 11
	s_add_u32 s6, s0, s6
	v_mov_b32_e32 v80, v0
	s_addc_u32 s7, s1, s7
	s_add_u32 s6, s6, s33
	v_readfirstlane_b32 s31, v80
	s_addc_u32 s7, s7, 0
	s_ashr_i32 s31, s31, 1
	v_lshrrev_b32_e32 v2, 1, v80
	s_andn2_b32 s31, s31, 31
	v_and_b32_e32 v72, 16, v2
	v_or_b32_e32 v2, s31, v72
	v_ashrrev_i32_e32 v3, 31, v2
	v_lshlrev_b32_e32 v4, 2, v80
	v_lshlrev_b64 v[2:3], 13, v[2:3]
	v_and_b32_e32 v73, 0x7c, v4
	v_lshl_add_u64 v[2:3], s[50:51], 0, v[2:3]
	v_lshlrev_b32_e32 v62, 2, v73
	v_lshl_add_u64 v[58:59], v[2:3], 0, v[62:63]
	v_add_co_u32_e32 v6, vcc, s14, v58
	s_nop 1
	v_addc_co_u32_e32 v7, vcc, 0, v59, vcc
	v_add_co_u32_e32 v10, vcc, s15, v58
	s_barrier
	s_nop 0
	v_addc_co_u32_e32 v11, vcc, 0, v59, vcc
	v_add_co_u32_e32 v12, vcc, s16, v58
	s_nop 1
	v_addc_co_u32_e32 v13, vcc, 0, v59, vcc
	v_add_co_u32_e32 v14, vcc, s17, v58
	global_load_dwordx4 v[2:5], v[58:59], off sc0 nt
	s_nop 0
	global_load_dwordx4 v[6:9], v[6:7], off sc0 nt
	v_addc_co_u32_e32 v15, vcc, 0, v59, vcc
	v_add_co_u32_e32 v22, vcc, s18, v58
	global_load_dwordx4 v[18:21], v[10:11], off sc0 nt
	s_nop 0
	global_load_dwordx4 v[10:13], v[12:13], off sc0 nt
	v_addc_co_u32_e32 v23, vcc, 0, v59, vcc
	v_add_co_u32_e32 v26, vcc, s19, v58
	global_load_dwordx4 v[14:17], v[14:15], off sc0 nt
	s_nop 0
	global_load_dwordx4 v[22:25], v[22:23], off sc0 nt
	v_addc_co_u32_e32 v27, vcc, 0, v59, vcc
	v_add_co_u32_e32 v28, vcc, s20, v58
	v_mov_b32_e32 v68, v63
	s_nop 0
	v_addc_co_u32_e32 v29, vcc, 0, v59, vcc
	v_add_co_u32_e32 v30, vcc, s21, v58
	global_load_dwordx4 v[34:37], v[26:27], off sc0 nt
	s_nop 0
	global_load_dwordx4 v[26:29], v[28:29], off sc0 nt
	v_addc_co_u32_e32 v31, vcc, 0, v59, vcc
	v_add_co_u32_e32 v38, vcc, s22, v58
	v_mov_b32_e32 v69, v63
	s_nop 0
	v_addc_co_u32_e32 v39, vcc, 0, v59, vcc
	v_add_co_u32_e32 v42, vcc, s23, v58
	global_load_dwordx4 v[30:33], v[30:31], off sc0 nt
	s_nop 0
	global_load_dwordx4 v[38:41], v[38:39], off sc0 nt
	v_addc_co_u32_e32 v43, vcc, 0, v59, vcc
	v_add_co_u32_e32 v44, vcc, s24, v58
	v_mov_b32_e32 v70, v63
	s_nop 0
	v_addc_co_u32_e32 v45, vcc, 0, v59, vcc
	v_add_co_u32_e32 v46, vcc, s25, v58
	global_load_dwordx4 v[50:53], v[42:43], off sc0 nt
	s_nop 0
	global_load_dwordx4 v[42:45], v[44:45], off sc0 nt
	v_addc_co_u32_e32 v47, vcc, 0, v59, vcc
	v_add_co_u32_e32 v54, vcc, s26, v58
	v_mov_b32_e32 v71, v63
	s_nop 0
	v_addc_co_u32_e32 v55, vcc, 0, v59, vcc
	global_load_dwordx4 v[46:49], v[46:47], off sc0 nt
	s_nop 0
	global_load_dwordx4 v[54:57], v[54:55], off sc0 nt
	v_add_co_u32_e32 v60, vcc, s27, v58
	s_add_i32 s31, s31, 0
	s_nop 0
	v_addc_co_u32_e32 v61, vcc, 0, v59, vcc
	v_add_co_u32_e32 v58, vcc, s28, v58
	global_load_dwordx4 v[64:67], v[60:61], off sc0 nt
	s_nop 0
	v_addc_co_u32_e32 v59, vcc, 0, v59, vcc
	global_load_dwordx4 v[58:61], v[58:59], off sc0 nt
	v_mov_b32_e32 v74, v63
	v_mov_b32_e32 v75, v63
	v_mov_b32_e32 v76, v63
	v_mov_b32_e32 v77, v63
	v_mov_b32_e32 v78, v63
	v_mov_b32_e32 v79, v63
	v_readlane_b32 s37, v254, 31
	v_readlane_b32 s38, v254, 32
	v_readlane_b32 s39, v254, 33
	v_readlane_b32 s40, v254, 34
	v_readlane_b32 s41, v254, 35
	v_readlane_b32 s42, v254, 36
	v_readlane_b32 s43, v254, 37
	v_readlane_b32 s44, v254, 38
	v_readlane_b32 s45, v254, 39
	v_readlane_b32 s48, v254, 42
	v_readlane_b32 s49, v254, 43
	s_waitcnt vmcnt(15)
	v_mul_f32_e32 v2, 0x43800000, v2
	s_waitcnt vmcnt(14)
	v_mul_f32_e32 v6, 0x43800000, v6
	v_med3_f32 v2, v2, s29, v1
	v_med3_f32 v6, v6, s29, v1
	v_cvt_pk_fp8_f32 v68, v2, v6
	s_waitcnt vmcnt(13)
	v_mul_f32_e32 v18, 0x43800000, v18
	s_waitcnt vmcnt(12)
	v_mul_f32_e32 v2, 0x43800000, v10
	v_med3_f32 v6, v18, s29, v1
	v_med3_f32 v2, v2, s29, v1
	v_cvt_pk_fp8_f32 v68, v6, v2 op_sel:[0,0,1]
	s_waitcnt vmcnt(11)
	v_mul_f32_e32 v2, 0x43800000, v14
	s_waitcnt vmcnt(10)
	v_mul_f32_e32 v6, 0x43800000, v22
	v_med3_f32 v2, v2, s29, v1
	v_med3_f32 v6, v6, s29, v1
	v_cvt_pk_fp8_f32 v69, v2, v6
	s_waitcnt vmcnt(9)
	v_mul_f32_e32 v10, 0x43800000, v34
	s_waitcnt vmcnt(8)
	v_mul_f32_e32 v2, 0x43800000, v26
	v_med3_f32 v6, v10, s29, v1
	v_med3_f32 v2, v2, s29, v1
	v_cvt_pk_fp8_f32 v69, v6, v2 op_sel:[0,0,1]
	s_waitcnt vmcnt(7)
	v_mul_f32_e32 v2, 0x43800000, v30
	s_waitcnt vmcnt(6)
	v_mul_f32_e32 v6, 0x43800000, v38
	v_med3_f32 v2, v2, s29, v1
	v_med3_f32 v6, v6, s29, v1
	v_cvt_pk_fp8_f32 v70, v2, v6
	s_waitcnt vmcnt(5)
	v_mul_f32_e32 v10, 0x43800000, v50
	s_waitcnt vmcnt(4)
	v_mul_f32_e32 v2, 0x43800000, v42
	v_med3_f32 v6, v10, s29, v1
	v_med3_f32 v2, v2, s29, v1
	v_cvt_pk_fp8_f32 v70, v6, v2 op_sel:[0,0,1]
	s_waitcnt vmcnt(3)
	v_mul_f32_e32 v2, 0x43800000, v46
	s_waitcnt vmcnt(2)
	v_mul_f32_e32 v6, 0x43800000, v54
	v_med3_f32 v2, v2, s29, v1
	v_med3_f32 v6, v6, s29, v1
	v_cvt_pk_fp8_f32 v71, v2, v6
	s_waitcnt vmcnt(1)
	v_mul_f32_e32 v10, 0x43800000, v64
	v_med3_f32 v6, v10, s29, v1
	s_waitcnt vmcnt(0)
	v_mul_f32_e32 v2, 0x43800000, v58
	v_med3_f32 v2, v2, s29, v1
	v_cvt_pk_fp8_f32 v71, v6, v2 op_sel:[0,0,1]
	v_mul_u32_u24_e32 v2, 0x110, v73
	v_add3_u32 v6, s31, v72, v2
	v_mul_f32_e32 v2, 0x43800000, v3
	v_mul_f32_e32 v3, 0x43800000, v7
	v_med3_f32 v2, v2, s29, v1
	v_med3_f32 v3, v3, s29, v1
	v_mov_b32_e32 v72, v63
	v_cvt_pk_fp8_f32 v72, v2, v3
	v_mul_f32_e32 v7, 0x43800000, v19
	v_mul_f32_e32 v2, 0x43800000, v11
	v_med3_f32 v3, v7, s29, v1
	v_med3_f32 v2, v2, s29, v1
	v_cvt_pk_fp8_f32 v72, v3, v2 op_sel:[0,0,1]
	v_mul_f32_e32 v2, 0x43800000, v15
	v_mul_f32_e32 v3, 0x43800000, v23
	v_med3_f32 v2, v2, s29, v1
	v_med3_f32 v3, v3, s29, v1
	v_mov_b32_e32 v73, v63
	v_cvt_pk_fp8_f32 v73, v2, v3
	v_mul_f32_e32 v7, 0x43800000, v35
	v_mul_f32_e32 v2, 0x43800000, v27
	v_med3_f32 v3, v7, s29, v1
	v_med3_f32 v2, v2, s29, v1
	v_cvt_pk_fp8_f32 v73, v3, v2 op_sel:[0,0,1]
	v_mul_f32_e32 v2, 0x43800000, v31
	v_mul_f32_e32 v3, 0x43800000, v39
	v_med3_f32 v2, v2, s29, v1
	v_med3_f32 v3, v3, s29, v1
	v_cvt_pk_fp8_f32 v74, v2, v3
	v_mul_f32_e32 v7, 0x43800000, v51
	v_mul_f32_e32 v2, 0x43800000, v43
	v_med3_f32 v3, v7, s29, v1
	v_med3_f32 v2, v2, s29, v1
	v_cvt_pk_fp8_f32 v74, v3, v2 op_sel:[0,0,1]
	v_mul_f32_e32 v2, 0x43800000, v47
	v_mul_f32_e32 v3, 0x43800000, v55
	v_med3_f32 v2, v2, s29, v1
	v_med3_f32 v3, v3, s29, v1
	v_cvt_pk_fp8_f32 v75, v2, v3
	v_mul_f32_e32 v7, 0x43800000, v65
	v_mul_f32_e32 v2, 0x43800000, v59
	v_med3_f32 v3, v7, s29, v1
	v_med3_f32 v2, v2, s29, v1
	v_cvt_pk_fp8_f32 v75, v3, v2 op_sel:[0,0,1]
	v_mul_f32_e32 v2, 0x43800000, v4
	v_mul_f32_e32 v3, 0x43800000, v8
	v_med3_f32 v2, v2, s29, v1
	v_med3_f32 v3, v3, s29, v1
	v_cvt_pk_fp8_f32 v76, v2, v3
	v_mul_f32_e32 v4, 0x43800000, v20
	v_mul_f32_e32 v2, 0x43800000, v12
	v_med3_f32 v3, v4, s29, v1
	v_med3_f32 v2, v2, s29, v1
	v_cvt_pk_fp8_f32 v76, v3, v2 op_sel:[0,0,1]
	v_mul_f32_e32 v2, 0x43800000, v16
	v_mul_f32_e32 v3, 0x43800000, v24
	v_med3_f32 v2, v2, s29, v1
	v_med3_f32 v3, v3, s29, v1
	v_cvt_pk_fp8_f32 v77, v2, v3
	v_mul_f32_e32 v4, 0x43800000, v36
	v_mul_f32_e32 v2, 0x43800000, v28
	v_med3_f32 v3, v4, s29, v1
	v_med3_f32 v2, v2, s29, v1
	v_cvt_pk_fp8_f32 v77, v3, v2 op_sel:[0,0,1]
	v_mul_f32_e32 v2, 0x43800000, v32
	v_mul_f32_e32 v3, 0x43800000, v40
	v_med3_f32 v2, v2, s29, v1
	v_med3_f32 v3, v3, s29, v1
	v_cvt_pk_fp8_f32 v78, v2, v3
	v_mul_f32_e32 v4, 0x43800000, v52
	v_mul_f32_e32 v2, 0x43800000, v44
	v_med3_f32 v3, v4, s29, v1
	v_med3_f32 v2, v2, s29, v1
	v_cvt_pk_fp8_f32 v78, v3, v2 op_sel:[0,0,1]
	v_mul_f32_e32 v2, 0x43800000, v48
	v_mul_f32_e32 v3, 0x43800000, v56
	v_med3_f32 v2, v2, s29, v1
	v_med3_f32 v3, v3, s29, v1
	v_cvt_pk_fp8_f32 v79, v2, v3
	v_mul_f32_e32 v4, 0x43800000, v66
	v_mul_f32_e32 v2, 0x43800000, v60
	v_med3_f32 v3, v4, s29, v1
	v_med3_f32 v2, v2, s29, v1
	v_cvt_pk_fp8_f32 v79, v3, v2 op_sel:[0,0,1]
	v_mul_f32_e32 v2, 0x43800000, v5
	v_mul_f32_e32 v3, 0x43800000, v9
	v_med3_f32 v5, v2, s29, v1
	v_med3_f32 v3, v3, s29, v1
	v_mov_b32_e32 v2, v63
	v_cvt_pk_fp8_f32 v2, v5, v3
	v_mul_f32_e32 v4, 0x43800000, v21
	v_mul_f32_e32 v3, 0x43800000, v13
	v_med3_f32 v4, v4, s29, v1
	v_med3_f32 v3, v3, s29, v1
	v_cvt_pk_fp8_f32 v2, v4, v3 op_sel:[0,0,1]
	v_mul_f32_e32 v3, 0x43800000, v17
	v_mul_f32_e32 v4, 0x43800000, v25
	v_med3_f32 v7, v3, s29, v1
	v_med3_f32 v4, v4, s29, v1
	v_mov_b32_e32 v3, v63
	v_cvt_pk_fp8_f32 v3, v7, v4
	v_mul_f32_e32 v5, 0x43800000, v37
	v_mul_f32_e32 v4, 0x43800000, v29
	v_med3_f32 v5, v5, s29, v1
	v_med3_f32 v4, v4, s29, v1
	v_cvt_pk_fp8_f32 v3, v5, v4 op_sel:[0,0,1]
	v_mul_f32_e32 v4, 0x43800000, v33
	v_mul_f32_e32 v5, 0x43800000, v41
	v_med3_f32 v8, v4, s29, v1
	v_med3_f32 v5, v5, s29, v1
	v_mov_b32_e32 v4, v63
	v_cvt_pk_fp8_f32 v4, v8, v5
	v_mul_f32_e32 v7, 0x43800000, v53
	v_mul_f32_e32 v5, 0x43800000, v45
	v_med3_f32 v7, v7, s29, v1
	v_med3_f32 v5, v5, s29, v1
	v_cvt_pk_fp8_f32 v4, v7, v5 op_sel:[0,0,1]
	v_mul_f32_e32 v5, 0x43800000, v49
	v_mul_f32_e32 v7, 0x43800000, v57
	v_med3_f32 v9, v5, s29, v1
	v_med3_f32 v7, v7, s29, v1
	v_mov_b32_e32 v5, v63
	v_cvt_pk_fp8_f32 v5, v9, v7
	v_mul_f32_e32 v8, 0x43800000, v67
	v_mul_f32_e32 v7, 0x43800000, v61
	v_med3_f32 v8, v8, s29, v1
	v_med3_f32 v7, v7, s29, v1
	v_cvt_pk_fp8_f32 v5, v8, v7 op_sel:[0,0,1]
	ds_write_b128 v6, v[68:71]
	ds_write_b128 v6, v[72:75] offset:272
	ds_write_b128 v6, v[76:79] offset:544
	ds_write_b128 v6, v[2:5] offset:816
	v_lshlrev_b32_e32 v2, 4, v80
	v_and_b32_e32 v62, 0xf0, v2
	v_ashrrev_i32_e32 v6, 4, v80
	v_add_u32_e32 v10, 0, v62
	v_ashrrev_i32_e32 v7, 31, v6
	v_lshl_add_u64 v[12:13], s[6:7], 0, v[62:63]
	v_mad_u64_u32 v[2:3], s[6:7], v6, s30, v[10:11]
	v_lshlrev_b64 v[6:7], 11, v[6:7]
	v_lshl_add_u64 v[14:15], v[12:13], 0, v[6:7]
	v_add_u32_e32 v6, 0x200, v80
	s_waitcnt lgkmcnt(0)
	s_barrier
	ds_read_b128 v[2:5], v2
	v_ashrrev_i32_e32 v16, 4, v6
	v_mad_u64_u32 v[6:7], s[6:7], v16, s30, v[10:11]
	ds_read_b128 v[6:9], v6
	v_ashrrev_i32_e32 v17, 31, v16
	s_waitcnt lgkmcnt(1)
	global_store_dwordx4 v[14:15], v[2:5], off
	s_nop 1
	v_lshlrev_b64 v[2:3], 11, v[16:17]
	v_lshl_add_u64 v[2:3], v[12:13], 0, v[2:3]
	s_waitcnt lgkmcnt(0)
	global_store_dwordx4 v[2:3], v[6:9], off
	v_add_u32_e32 v2, 0x400, v80
	s_nop 0
	v_ashrrev_i32_e32 v6, 4, v2
	v_ashrrev_i32_e32 v7, 31, v6
	v_mad_u64_u32 v[2:3], s[6:7], v6, s30, v[10:11]
	v_lshlrev_b64 v[6:7], 11, v[6:7]
	v_lshl_add_u64 v[14:15], v[12:13], 0, v[6:7]
	v_add_u32_e32 v6, 0x600, v80
	ds_read_b128 v[2:5], v2
	v_ashrrev_i32_e32 v16, 4, v6
	v_mad_u64_u32 v[6:7], s[6:7], v16, s30, v[10:11]
	ds_read_b128 v[6:9], v6
	v_ashrrev_i32_e32 v17, 31, v16
	s_waitcnt lgkmcnt(1)
	global_store_dwordx4 v[14:15], v[2:5], off
	s_nop 1
	v_lshlrev_b64 v[2:3], 11, v[16:17]
	v_lshl_add_u64 v[2:3], v[12:13], 0, v[2:3]
	s_waitcnt lgkmcnt(0)
	global_store_dwordx4 v[2:3], v[6:9], off
	s_barrier
	s_branch .LBB0_25

.LBB0_98:
	s_addk_i32 s2, 0x100
	s_and_b32 s24, s3, 0x700
	s_ashr_i32 s25, s2, 3
	s_mul_i32 s26, s24, 0xa040
	s_add_u32 s31, s46, s26
	s_addc_u32 s33, s47, 0
	s_lshl_b32 s26, s25, 7
	s_ashr_i32 s27, s26, 31
	s_lshl_b64 s[28:29], s[26:27], 2
	s_add_u32 s28, s31, s28
	s_addc_u32 s29, s33, s29
	s_cmp_gt_i32 s25, 23
	s_cselect_b32 s25, 64, 0
	s_add_u32 s28, s28, s25
	s_addc_u32 s29, s29, 0
	s_lshl_b64 s[26:27], s[26:27], 11
	s_add_u32 s25, s0, s26
	v_mov_b32_e32 v18, v0
	s_addc_u32 s26, s1, s27
	s_add_u32 s24, s25, s24
	v_readfirstlane_b32 s30, v18
	v_lshrrev_b32_e32 v20, 1, v18
	v_lshlrev_b32_e32 v21, 2, v18
	s_addc_u32 s25, s26, 0
	s_ashr_i32 s26, s30, 1
	v_lshlrev_b32_e32 v22, 4, v18
	v_ashrrev_i32_e32 v84, 4, v18
	v_add_u32_e32 v23, 0x200, v18
	v_add_u32_e32 v24, 0x400, v18
	v_add_u32_e32 v18, 0x600, v18
	v_and_b32_e32 v25, 16, v20
	v_and_b32_e32 v20, 0x7c, v21
	s_andn2_b32 s26, s26, 31
	v_ashrrev_i32_e32 v86, 4, v23
	v_ashrrev_i32_e32 v88, 4, v24
	v_ashrrev_i32_e32 v90, 4, v18
	v_lshlrev_b32_e32 v18, 2, v20
	v_mul_u32_u24_e32 v23, 0x110, v20
	v_mov_b64_e32 v[20:21], s[28:29]
	v_or_b32_e32 v24, s26, v25
	s_add_i32 s28, s26, 0
	v_mad_i64_i32 v[20:21], s[26:27], v24, s4, v[20:21]
	v_add3_u32 v101, s28, v25, v23
	v_lshl_add_u64 v[24:25], v[20:21], 0, v[18:19]
	v_add_co_u32_e32 v26, vcc, s5, v24
	s_waitcnt lgkmcnt(0)
	s_nop 0
	v_addc_co_u32_e32 v27, vcc, 0, v25, vcc
	v_add_co_u32_e32 v28, vcc, s8, v24
	s_barrier
	s_nop 0
	v_addc_co_u32_e32 v29, vcc, 0, v25, vcc
	v_add_co_u32_e32 v32, vcc, s9, v24
	s_nop 1
	v_addc_co_u32_e32 v33, vcc, 0, v25, vcc
	v_add_co_u32_e32 v36, vcc, s10, v24
	v_and_b32_e32 v18, 0xf0, v22
	s_nop 0
	v_addc_co_u32_e32 v37, vcc, 0, v25, vcc
	v_add_co_u32_e32 v40, vcc, s11, v24
	global_load_dwordx4 v[20:23], v[24:25], off sc0 nt
	s_nop 0
	v_addc_co_u32_e32 v41, vcc, 0, v25, vcc
	v_add_co_u32_e32 v44, vcc, s12, v24
	v_add_u32_e32 v100, 0, v18
	s_nop 0
	v_addc_co_u32_e32 v45, vcc, 0, v25, vcc
	v_add_co_u32_e32 v48, vcc, s13, v24
	v_lshl_add_u64 v[102:103], s[24:25], 0, v[18:19]
	s_nop 0
	v_addc_co_u32_e32 v49, vcc, 0, v25, vcc
	v_add_co_u32_e32 v52, vcc, s14, v24
	v_mov_b32_e32 v2, v19
	s_nop 0
	v_addc_co_u32_e32 v53, vcc, 0, v25, vcc
	v_add_co_u32_e32 v56, vcc, s15, v24
	v_mov_b32_e32 v3, v19
	s_nop 0
	v_addc_co_u32_e32 v57, vcc, 0, v25, vcc
	v_add_co_u32_e32 v60, vcc, s16, v24
	v_mov_b32_e32 v4, v19
	s_nop 0
	v_addc_co_u32_e32 v61, vcc, 0, v25, vcc
	v_add_co_u32_e32 v64, vcc, s17, v24
	v_mov_b32_e32 v5, v19
	s_nop 0
	v_addc_co_u32_e32 v65, vcc, 0, v25, vcc
	v_add_co_u32_e32 v68, vcc, s18, v24
	v_mov_b32_e32 v6, v19
	s_nop 0
	v_addc_co_u32_e32 v69, vcc, 0, v25, vcc
	v_add_co_u32_e32 v72, vcc, s19, v24
	v_mov_b32_e32 v7, v19
	s_nop 0
	v_addc_co_u32_e32 v73, vcc, 0, v25, vcc
	v_add_co_u32_e32 v76, vcc, s20, v24
	v_mov_b32_e32 v8, v19
	s_nop 0
	v_addc_co_u32_e32 v77, vcc, 0, v25, vcc
	v_add_co_u32_e32 v80, vcc, s21, v24
	v_mov_b32_e32 v9, v19
	s_nop 0
	v_addc_co_u32_e32 v81, vcc, 0, v25, vcc
	global_load_dwordx4 v[24:27], v[26:27], off offset:64 sc0 nt
	s_nop 0
	global_load_dwordx4 v[28:31], v[28:29], off offset:128 sc0 nt
	s_nop 0
	global_load_dwordx4 v[32:35], v[32:33], off offset:192 sc0 nt
	s_nop 0
	global_load_dwordx4 v[36:39], v[36:37], off offset:256 sc0 nt
	s_nop 0
	global_load_dwordx4 v[40:43], v[40:41], off offset:320 sc0 nt
	s_nop 0
	global_load_dwordx4 v[44:47], v[44:45], off offset:384 sc0 nt
	s_nop 0
	global_load_dwordx4 v[48:51], v[48:49], off offset:448 sc0 nt
	s_nop 0
	global_load_dwordx4 v[52:55], v[52:53], off offset:512 sc0 nt
	s_nop 0
	global_load_dwordx4 v[56:59], v[56:57], off offset:576 sc0 nt
	s_nop 0
	global_load_dwordx4 v[60:63], v[60:61], off offset:640 sc0 nt
	s_nop 0
	global_load_dwordx4 v[64:67], v[64:65], off offset:704 sc0 nt
	s_nop 0
	global_load_dwordx4 v[68:71], v[68:69], off offset:768 sc0 nt
	s_nop 0
	global_load_dwordx4 v[72:75], v[72:73], off offset:832 sc0 nt
	s_nop 0
	global_load_dwordx4 v[76:79], v[76:77], off offset:896 sc0 nt
	s_nop 0
	global_load_dwordx4 v[80:83], v[80:81], off offset:960 sc0 nt
	v_mov_b32_e32 v10, v19
	v_mov_b32_e32 v11, v19
	v_mov_b32_e32 v12, v19
	v_mov_b32_e32 v13, v19
	v_mov_b32_e32 v14, v19
	v_mov_b32_e32 v15, v19
	v_mov_b32_e32 v16, v19
	v_mov_b32_e32 v17, v19
	v_ashrrev_i32_e32 v85, 31, v84
	v_lshlrev_b64 v[92:93], 11, v[84:85]
	v_ashrrev_i32_e32 v87, 31, v86
	v_ashrrev_i32_e32 v89, 31, v88
	v_ashrrev_i32_e32 v91, 31, v90
	v_mad_u64_u32 v[84:85], s[24:25], v84, s23, v[100:101]
	v_lshlrev_b64 v[94:95], 11, v[86:87]
	v_lshlrev_b64 v[96:97], 11, v[88:89]
	v_lshlrev_b64 v[98:99], 11, v[90:91]
	v_mad_u64_u32 v[86:87], s[24:25], v86, s23, v[100:101]
	v_mad_u64_u32 v[88:89], s[24:25], v88, s23, v[100:101]
	v_mad_u64_u32 v[90:91], s[24:25], v90, s23, v[100:101]
	s_add_i32 s3, s3, 0x10000
	s_cmpk_lt_i32 s2, 0x180
	s_waitcnt vmcnt(15)
	v_mul_f32_e32 v18, 0x43800000, v20
	v_mul_f32_e32 v20, 0x43800000, v21
	v_mul_f32_e32 v21, 0x43800000, v22
	v_mul_f32_e32 v22, 0x43800000, v23
	v_med3_f32 v18, v18, s22, v1
	v_med3_f32 v20, v20, s22, v1
	v_med3_f32 v21, v21, s22, v1
	v_med3_f32 v22, v22, s22, v1
	v_lshl_add_u64 v[92:93], v[102:103], 0, v[92:93]
	v_lshl_add_u64 v[94:95], v[102:103], 0, v[94:95]
	v_lshl_add_u64 v[96:97], v[102:103], 0, v[96:97]
	v_lshl_add_u64 v[98:99], v[102:103], 0, v[98:99]
	s_waitcnt vmcnt(14)
	v_mul_f32_e32 v23, 0x43800000, v24
	s_waitcnt vmcnt(13)
	v_mul_f32_e32 v24, 0x43800000, v28
	s_waitcnt vmcnt(12)
	v_mul_f32_e32 v28, 0x43800000, v32
	s_waitcnt vmcnt(11)
	v_mul_f32_e32 v32, 0x43800000, v36
	s_waitcnt vmcnt(10)
	v_mul_f32_e32 v36, 0x43800000, v40
	s_waitcnt vmcnt(9)
	v_mul_f32_e32 v40, 0x43800000, v44
	s_waitcnt vmcnt(8)
	v_mul_f32_e32 v44, 0x43800000, v48
	s_waitcnt vmcnt(7)
	v_mul_f32_e32 v48, 0x43800000, v52
	s_waitcnt vmcnt(6)
	v_mul_f32_e32 v52, 0x43800000, v56
	s_waitcnt vmcnt(5)
	v_mul_f32_e32 v56, 0x43800000, v60
	s_waitcnt vmcnt(4)
	v_mul_f32_e32 v60, 0x43800000, v64
	s_waitcnt vmcnt(3)
	v_mul_f32_e32 v64, 0x43800000, v68
	s_waitcnt vmcnt(2)
	v_mul_f32_e32 v68, 0x43800000, v72
	v_mul_f32_e32 v25, 0x43800000, v25
	v_mul_f32_e32 v37, 0x43800000, v37
	v_mul_f32_e32 v41, 0x43800000, v41
	v_mul_f32_e32 v53, 0x43800000, v53
	v_mul_f32_e32 v57, 0x43800000, v57
	v_mul_f32_e32 v69, 0x43800000, v69
	v_mul_f32_e32 v73, 0x43800000, v73
	v_med3_f32 v23, v23, s22, v1
	v_med3_f32 v32, v32, s22, v1
	v_med3_f32 v36, v36, s22, v1
	v_med3_f32 v48, v48, s22, v1
	v_med3_f32 v52, v52, s22, v1
	v_med3_f32 v64, v64, s22, v1
	v_med3_f32 v68, v68, s22, v1
	v_mul_f32_e32 v26, 0x43800000, v26
	v_mul_f32_e32 v38, 0x43800000, v38
	v_mul_f32_e32 v42, 0x43800000, v42
	v_mul_f32_e32 v54, 0x43800000, v54
	v_mul_f32_e32 v58, 0x43800000, v58
	v_mul_f32_e32 v70, 0x43800000, v70
	v_mul_f32_e32 v74, 0x43800000, v74
	v_med3_f32 v25, v25, s22, v1
	v_med3_f32 v37, v37, s22, v1
	v_med3_f32 v41, v41, s22, v1
	v_med3_f32 v53, v53, s22, v1
	v_med3_f32 v57, v57, s22, v1
	v_med3_f32 v69, v69, s22, v1
	v_med3_f32 v73, v73, s22, v1
	v_cvt_pk_fp8_f32 v2, v18, v23
	v_cvt_pk_fp8_f32 v3, v32, v36
	v_cvt_pk_fp8_f32 v4, v48, v52
	v_cvt_pk_fp8_f32 v5, v64, v68
	v_mul_f32_e32 v27, 0x43800000, v27
	v_mul_f32_e32 v39, 0x43800000, v39
	v_mul_f32_e32 v43, 0x43800000, v43
	v_mul_f32_e32 v55, 0x43800000, v55
	v_mul_f32_e32 v59, 0x43800000, v59
	v_mul_f32_e32 v71, 0x43800000, v71
	v_mul_f32_e32 v75, 0x43800000, v75
	v_med3_f32 v26, v26, s22, v1
	v_med3_f32 v38, v38, s22, v1
	v_med3_f32 v42, v42, s22, v1
	v_med3_f32 v54, v54, s22, v1
	v_med3_f32 v58, v58, s22, v1
	v_med3_f32 v70, v70, s22, v1
	v_med3_f32 v74, v74, s22, v1
	v_cvt_pk_fp8_f32 v6, v20, v25
	v_cvt_pk_fp8_f32 v7, v37, v41
	v_cvt_pk_fp8_f32 v8, v53, v57
	v_cvt_pk_fp8_f32 v9, v69, v73
	s_waitcnt vmcnt(1)
	v_mul_f32_e32 v72, 0x43800000, v76
	s_waitcnt vmcnt(0)
	v_mul_f32_e32 v76, 0x43800000, v80
	v_med3_f32 v27, v27, s22, v1
	v_med3_f32 v39, v39, s22, v1
	v_med3_f32 v43, v43, s22, v1
	v_med3_f32 v55, v55, s22, v1
	v_med3_f32 v59, v59, s22, v1
	v_med3_f32 v71, v71, s22, v1
	v_med3_f32 v75, v75, s22, v1
	v_cvt_pk_fp8_f32 v10, v21, v26
	v_cvt_pk_fp8_f32 v11, v38, v42
	v_cvt_pk_fp8_f32 v12, v54, v58
	v_cvt_pk_fp8_f32 v13, v70, v74
	v_mul_f32_e32 v29, 0x43800000, v29
	v_mul_f32_e32 v33, 0x43800000, v33
	v_mul_f32_e32 v45, 0x43800000, v45
	v_mul_f32_e32 v49, 0x43800000, v49
	v_mul_f32_e32 v61, 0x43800000, v61
	v_mul_f32_e32 v65, 0x43800000, v65
	v_mul_f32_e32 v77, 0x43800000, v77
	v_mul_f32_e32 v80, 0x43800000, v81
	v_med3_f32 v24, v24, s22, v1
	v_med3_f32 v28, v28, s22, v1
	v_med3_f32 v40, v40, s22, v1
	v_med3_f32 v44, v44, s22, v1
	v_med3_f32 v56, v56, s22, v1
	v_med3_f32 v60, v60, s22, v1
	v_med3_f32 v72, v72, s22, v1
	v_med3_f32 v76, v76, s22, v1
	v_cvt_pk_fp8_f32 v14, v22, v27
	v_cvt_pk_fp8_f32 v15, v39, v43
	v_cvt_pk_fp8_f32 v16, v55, v59
	v_cvt_pk_fp8_f32 v17, v71, v75
	v_mul_f32_e32 v30, 0x43800000, v30
	v_mul_f32_e32 v34, 0x43800000, v34
	v_mul_f32_e32 v46, 0x43800000, v46
	v_mul_f32_e32 v50, 0x43800000, v50
	v_mul_f32_e32 v62, 0x43800000, v62
	v_mul_f32_e32 v66, 0x43800000, v66
	v_mul_f32_e32 v78, 0x43800000, v78
	v_mul_f32_e32 v81, 0x43800000, v82
	v_med3_f32 v29, v29, s22, v1
	v_med3_f32 v33, v33, s22, v1
	v_med3_f32 v45, v45, s22, v1
	v_med3_f32 v49, v49, s22, v1
	v_med3_f32 v61, v61, s22, v1
	v_med3_f32 v65, v65, s22, v1
	v_med3_f32 v77, v77, s22, v1
	v_med3_f32 v80, v80, s22, v1
	v_cvt_pk_fp8_f32 v2, v24, v28 op_sel:[0,0,1]
	v_cvt_pk_fp8_f32 v3, v40, v44 op_sel:[0,0,1]
	v_cvt_pk_fp8_f32 v4, v56, v60 op_sel:[0,0,1]
	v_cvt_pk_fp8_f32 v5, v72, v76 op_sel:[0,0,1]
	v_mul_f32_e32 v31, 0x43800000, v31
	v_mul_f32_e32 v35, 0x43800000, v35
	v_mul_f32_e32 v47, 0x43800000, v47
	v_mul_f32_e32 v51, 0x43800000, v51
	v_mul_f32_e32 v63, 0x43800000, v63
	v_mul_f32_e32 v67, 0x43800000, v67
	v_mul_f32_e32 v79, 0x43800000, v79
	v_mul_f32_e32 v82, 0x43800000, v83
	v_med3_f32 v30, v30, s22, v1
	v_med3_f32 v34, v34, s22, v1
	v_med3_f32 v46, v46, s22, v1
	v_med3_f32 v50, v50, s22, v1
	v_med3_f32 v62, v62, s22, v1
	v_med3_f32 v66, v66, s22, v1
	v_med3_f32 v78, v78, s22, v1
	v_med3_f32 v81, v81, s22, v1
	v_cvt_pk_fp8_f32 v6, v29, v33 op_sel:[0,0,1]
	v_cvt_pk_fp8_f32 v7, v45, v49 op_sel:[0,0,1]
	v_cvt_pk_fp8_f32 v8, v61, v65 op_sel:[0,0,1]
	v_cvt_pk_fp8_f32 v9, v77, v80 op_sel:[0,0,1]
	v_med3_f32 v31, v31, s22, v1
	v_med3_f32 v35, v35, s22, v1
	v_med3_f32 v47, v47, s22, v1
	v_med3_f32 v51, v51, s22, v1
	v_med3_f32 v63, v63, s22, v1
	v_med3_f32 v67, v67, s22, v1
	v_med3_f32 v79, v79, s22, v1
	v_med3_f32 v82, v82, s22, v1
	v_cvt_pk_fp8_f32 v10, v30, v34 op_sel:[0,0,1]
	v_cvt_pk_fp8_f32 v11, v46, v50 op_sel:[0,0,1]
	v_cvt_pk_fp8_f32 v12, v62, v66 op_sel:[0,0,1]
	v_cvt_pk_fp8_f32 v13, v78, v81 op_sel:[0,0,1]
	v_cvt_pk_fp8_f32 v14, v31, v35 op_sel:[0,0,1]
	v_cvt_pk_fp8_f32 v15, v47, v51 op_sel:[0,0,1]
	v_cvt_pk_fp8_f32 v16, v63, v67 op_sel:[0,0,1]
	v_cvt_pk_fp8_f32 v17, v79, v82 op_sel:[0,0,1]
	ds_write_b128 v101, v[2:5]
	ds_write_b128 v101, v[6:9] offset:272
	ds_write_b128 v101, v[10:13] offset:544
	ds_write_b128 v101, v[14:17] offset:816
	s_waitcnt lgkmcnt(0)
	s_barrier
	ds_read_b128 v[2:5], v84
	ds_read_b128 v[6:9], v86
	ds_read_b128 v[10:13], v88
	ds_read_b128 v[14:17], v90
	s_waitcnt lgkmcnt(3)
	global_store_dwordx4 v[92:93], v[2:5], off
	s_waitcnt lgkmcnt(2)
	global_store_dwordx4 v[94:95], v[6:9], off
	s_waitcnt lgkmcnt(1)
	global_store_dwordx4 v[96:97], v[10:13], off
	s_waitcnt lgkmcnt(0)
	global_store_dwordx4 v[98:99], v[14:17], off
	s_barrier
	s_cbranch_scc1 .LBB0_98

.LBB0_163:
	s_cmpk_gt_i32 s76, 0x3ff
	s_mov_b64 s[10:11], -1
	s_cbranch_scc0 .LBB0_165
	s_add_i32 s2, s76, 0xfffffc00
	s_lshr_b32 s8, s2, 4
	v_readlane_b32 s84, v254, 4
	s_lshl_b64 s[10:11], s[8:9], 24
	v_readlane_b32 s90, v254, 10
	v_readlane_b32 s91, v254, 11
	s_add_u32 s10, s90, s10
	s_addc_u32 s11, s91, s11
	s_and_b32 s34, s6, 0x780
	s_lshl_b32 s35, s34, 2
	s_add_u32 s68, s10, s35
	s_addc_u32 s69, s11, 0
	s_lshl_b64 s[10:11], s[8:9], 22
	s_lshl_b32 s8, s34, 11
	s_add_u32 s10, s0, s10
	v_mov_b32_e32 v130, v0
	s_addc_u32 s11, s1, s11
	s_add_u32 s10, s10, s8
	v_readfirstlane_b32 s2, v130
	s_addc_u32 s11, s11, 0
	s_ashr_i32 s2, s2, 1
	s_waitcnt lgkmcnt(1)
	v_lshrrev_b32_e32 v2, 1, v130
	s_andn2_b32 s2, s2, 31
	v_and_b32_e32 v131, 16, v2
	v_or_b32_e32 v2, s2, v131
	v_ashrrev_i32_e32 v3, 31, v2
	s_waitcnt lgkmcnt(0)
	v_lshlrev_b32_e32 v4, 2, v130
	v_lshlrev_b64 v[2:3], 13, v[2:3]
	v_and_b32_e32 v136, 0x7c, v4
	v_lshl_add_u64 v[2:3], s[68:69], 0, v[2:3]
	v_lshlrev_b32_e32 v162, 2, v136
	v_lshl_add_u64 v[180:181], v[2:3], 0, v[162:163]
	s_movk_i32 s8, 0x2000
	v_add_co_u32_e32 v2, vcc, s8, v180
	s_movk_i32 s8, 0x6000
	s_nop 0
	v_addc_co_u32_e32 v3, vcc, 0, v181, vcc
	global_load_dwordx4 v[110:113], v[180:181], off sc0 nt
	global_load_dwordx4 v[118:121], v[2:3], off sc0 nt
	v_add_co_u32_e32 v2, vcc, s12, v180
	v_readlane_b32 s85, v254, 5
	s_nop 0
	v_addc_co_u32_e32 v3, vcc, 0, v181, vcc
	v_add_co_u32_e32 v4, vcc, s8, v180
	s_mov_b32 s8, 0xa000
	s_nop 0
	v_addc_co_u32_e32 v5, vcc, 0, v181, vcc
	global_load_dwordx4 v[122:125], v[2:3], off sc0 nt
	global_load_dwordx4 v[126:129], v[4:5], off sc0 nt
	v_add_co_u32_e32 v2, vcc, s13, v180
	v_readlane_b32 s86, v254, 6
	s_nop 0
	v_addc_co_u32_e32 v3, vcc, 0, v181, vcc
	v_add_co_u32_e32 v4, vcc, s8, v180
	s_mov_b32 s8, 0xe000
	s_nop 0
	v_addc_co_u32_e32 v5, vcc, 0, v181, vcc
	global_load_dwordx4 v[94:97], v[2:3], off sc0 nt
	global_load_dwordx4 v[102:105], v[4:5], off sc0 nt
	v_add_co_u32_e32 v2, vcc, s14, v180
	v_readlane_b32 s87, v254, 7
	s_nop 0
	v_addc_co_u32_e32 v3, vcc, 0, v181, vcc
	v_add_co_u32_e32 v4, vcc, s8, v180
	s_mov_b32 s8, 0x12000
	s_nop 0
	v_addc_co_u32_e32 v5, vcc, 0, v181, vcc
	global_load_dwordx4 v[106:109], v[2:3], off sc0 nt
	global_load_dwordx4 v[114:117], v[4:5], off sc0 nt
	v_add_co_u32_e32 v2, vcc, s15, v180
	v_readlane_b32 s88, v254, 8
	s_nop 0
	v_addc_co_u32_e32 v3, vcc, 0, v181, vcc
	v_add_co_u32_e32 v4, vcc, s8, v180
	s_mov_b32 s8, 0x16000
	s_nop 0
	v_addc_co_u32_e32 v5, vcc, 0, v181, vcc
	global_load_dwordx4 v[78:81], v[2:3], off sc0 nt
	global_load_dwordx4 v[86:89], v[4:5], off sc0 nt
	v_add_co_u32_e32 v2, vcc, s16, v180
	v_readlane_b32 s89, v254, 9
	s_nop 0
	v_addc_co_u32_e32 v3, vcc, 0, v181, vcc
	v_add_co_u32_e32 v4, vcc, s8, v180
	s_mov_b32 s8, 0x1a000
	s_nop 0
	v_addc_co_u32_e32 v5, vcc, 0, v181, vcc
	global_load_dwordx4 v[90:93], v[2:3], off sc0 nt
	global_load_dwordx4 v[98:101], v[4:5], off sc0 nt
	v_add_co_u32_e32 v2, vcc, s17, v180
	s_nop 1
	v_addc_co_u32_e32 v3, vcc, 0, v181, vcc
	v_add_co_u32_e32 v4, vcc, s8, v180
	s_mov_b32 s8, 0x1e000
	s_nop 0
	v_addc_co_u32_e32 v5, vcc, 0, v181, vcc
	global_load_dwordx4 v[66:69], v[2:3], off sc0 nt
	global_load_dwordx4 v[70:73], v[4:5], off sc0 nt
	v_add_co_u32_e32 v2, vcc, s18, v180
	s_nop 1
	v_addc_co_u32_e32 v3, vcc, 0, v181, vcc
	v_add_co_u32_e32 v4, vcc, s8, v180
	s_mov_b32 s8, 0x200000
	s_nop 0
	v_addc_co_u32_e32 v5, vcc, 0, v181, vcc
	global_load_dwordx4 v[74:77], v[2:3], off sc0 nt
	global_load_dwordx4 v[82:85], v[4:5], off sc0 nt
	v_add_co_u32_e32 v2, vcc, s8, v180
	s_mov_b32 s8, 0x202000
	s_nop 0
	v_addc_co_u32_e32 v3, vcc, 0, v181, vcc
	v_add_co_u32_e32 v4, vcc, s8, v180
	s_mov_b32 s8, 0x204000
	s_nop 0
	v_addc_co_u32_e32 v5, vcc, 0, v181, vcc
	global_load_dwordx4 v[50:53], v[2:3], off sc0 nt
	global_load_dwordx4 v[54:57], v[4:5], off sc0 nt
	v_add_co_u32_e32 v2, vcc, s8, v180
	s_mov_b32 s8, 0x206000
	s_nop 0
	v_addc_co_u32_e32 v3, vcc, 0, v181, vcc
	v_add_co_u32_e32 v4, vcc, s8, v180
	s_mov_b32 s8, 0x208000
	s_nop 0
	v_addc_co_u32_e32 v5, vcc, 0, v181, vcc
	global_load_dwordx4 v[62:65], v[2:3], off sc0 nt
	global_load_dwordx4 v[42:45], v[4:5], off sc0 nt
	v_add_co_u32_e32 v2, vcc, s8, v180
	s_mov_b32 s8, 0x20a000
	s_nop 0
	v_addc_co_u32_e32 v3, vcc, 0, v181, vcc
	v_add_co_u32_e32 v4, vcc, s8, v180
	s_mov_b32 s8, 0x20c000
	s_nop 0
	v_addc_co_u32_e32 v5, vcc, 0, v181, vcc
	global_load_dwordx4 v[34:37], v[2:3], off sc0 nt
	global_load_dwordx4 v[38:41], v[4:5], off sc0 nt
	v_add_co_u32_e32 v2, vcc, s8, v180
	s_mov_b32 s8, 0x20e000
	s_nop 0
	v_addc_co_u32_e32 v3, vcc, 0, v181, vcc
	v_add_co_u32_e32 v4, vcc, s8, v180
	s_mov_b32 s8, 0x210000
	s_nop 0
	v_addc_co_u32_e32 v5, vcc, 0, v181, vcc
	global_load_dwordx4 v[58:61], v[2:3], off sc0 nt
	global_load_dwordx4 v[26:29], v[4:5], off sc0 nt
	v_add_co_u32_e32 v2, vcc, s8, v180
	s_mov_b32 s8, 0x212000
	s_nop 0
	v_addc_co_u32_e32 v3, vcc, 0, v181, vcc
	v_add_co_u32_e32 v4, vcc, s8, v180
	s_mov_b32 s8, 0x214000
	s_nop 0
	v_addc_co_u32_e32 v5, vcc, 0, v181, vcc
	global_load_dwordx4 v[18:21], v[2:3], off sc0 nt
	global_load_dwordx4 v[22:25], v[4:5], off sc0 nt
	v_add_co_u32_e32 v2, vcc, s8, v180
	s_mov_b32 s8, 0x216000
	s_nop 0
	v_addc_co_u32_e32 v3, vcc, 0, v181, vcc
	v_add_co_u32_e32 v4, vcc, s8, v180
	s_mov_b32 s8, 0x218000
	s_nop 0
	v_addc_co_u32_e32 v5, vcc, 0, v181, vcc
	global_load_dwordx4 v[46:49], v[2:3], off sc0 nt
	global_load_dwordx4 v[14:17], v[4:5], off sc0 nt
	v_add_co_u32_e32 v2, vcc, s8, v180
	s_mov_b32 s8, 0x21a000
	s_nop 0
	v_addc_co_u32_e32 v3, vcc, 0, v181, vcc
	v_add_co_u32_e32 v4, vcc, s8, v180
	s_mov_b32 s8, 0x21c000
	s_nop 0
	v_addc_co_u32_e32 v5, vcc, 0, v181, vcc
	global_load_dwordx4 v[6:9], v[2:3], off sc0 nt
	global_load_dwordx4 v[10:13], v[4:5], off sc0 nt
	v_add_co_u32_e32 v2, vcc, s8, v180
	s_mov_b32 s8, 0x21e000
	s_nop 0
	v_addc_co_u32_e32 v3, vcc, 0, v181, vcc
	v_add_co_u32_e32 v4, vcc, s8, v180
	s_nop 1
	v_addc_co_u32_e32 v5, vcc, 0, v181, vcc
	global_load_dwordx4 v[30:33], v[2:3], off sc0 nt
	s_nop 0
	global_load_dwordx4 v[2:5], v[4:5], off sc0 nt
	s_waitcnt vmcnt(31)
	v_mul_f32_e32 v110, 0x43800000, v110
	s_waitcnt vmcnt(30)
	v_mul_f32_e32 v118, 0x43800000, v118
	s_waitcnt vmcnt(27)
	v_mul_f32_e32 v94, 0x43800000, v94
	s_waitcnt vmcnt(26)
	v_mul_f32_e32 v102, 0x43800000, v102
	s_waitcnt vmcnt(23)
	v_mul_f32_e32 v78, 0x43800000, v78
	s_waitcnt vmcnt(22)
	v_mul_f32_e32 v86, 0x43800000, v86
	s_waitcnt vmcnt(19)
	v_mul_f32_e32 v66, 0x43800000, v66
	s_waitcnt vmcnt(18)
	v_mul_f32_e32 v70, 0x43800000, v70
	v_med3_f32 v110, v110, s19, v1
	v_med3_f32 v118, v118, s19, v1
	v_mov_b32_e32 v132, v163
	v_med3_f32 v94, v94, s19, v1
	v_med3_f32 v102, v102, s19, v1
	v_mov_b32_e32 v133, v163
	v_med3_f32 v78, v78, s19, v1
	v_med3_f32 v86, v86, s19, v1
	v_mov_b32_e32 v134, v163
	v_med3_f32 v66, v66, s19, v1
	v_med3_f32 v70, v70, s19, v1
	v_mov_b32_e32 v135, v163
	v_cvt_pk_fp8_f32 v132, v110, v118
	v_cvt_pk_fp8_f32 v133, v94, v102
	v_cvt_pk_fp8_f32 v134, v78, v86
	v_cvt_pk_fp8_f32 v135, v66, v70
	v_mul_f32_e32 v122, 0x43800000, v122
	v_mul_f32_e32 v126, 0x43800000, v126
	v_mul_f32_e32 v106, 0x43800000, v106
	v_mul_f32_e32 v110, 0x43800000, v114
	v_mul_f32_e32 v90, 0x43800000, v90
	v_mul_f32_e32 v94, 0x43800000, v98
	s_waitcnt vmcnt(17)
	v_mul_f32_e32 v74, 0x43800000, v74
	s_waitcnt vmcnt(16)
	v_mul_f32_e32 v78, 0x43800000, v82
	v_med3_f32 v122, v122, s19, v1
	v_med3_f32 v126, v126, s19, v1
	v_med3_f32 v106, v106, s19, v1
	v_med3_f32 v110, v110, s19, v1
	v_med3_f32 v90, v90, s19, v1
	v_med3_f32 v94, v94, s19, v1
	v_med3_f32 v74, v74, s19, v1
	v_med3_f32 v78, v78, s19, v1
	v_cvt_pk_fp8_f32 v132, v122, v126 op_sel:[0,0,1]
	v_cvt_pk_fp8_f32 v133, v106, v110 op_sel:[0,0,1]
	v_cvt_pk_fp8_f32 v134, v90, v94 op_sel:[0,0,1]
	v_cvt_pk_fp8_f32 v135, v74, v78 op_sel:[0,0,1]
	s_add_i32 s2, s2, 0
	v_mul_u32_u24_e32 v66, 0x110, v136
	v_add3_u32 v182, s2, v131, v66
	v_mul_f32_e32 v66, 0x43800000, v111
	v_mul_f32_e32 v70, 0x43800000, v119
	ds_write_b128 v182, v[132:135]
	v_med3_f32 v66, v66, s19, v1
	v_med3_f32 v70, v70, s19, v1
	v_mov_b32_e32 v132, v163
	v_cvt_pk_fp8_f32 v132, v66, v70
	v_mul_f32_e32 v66, 0x43800000, v95
	v_mul_f32_e32 v70, 0x43800000, v103
	v_med3_f32 v66, v66, s19, v1
	v_med3_f32 v70, v70, s19, v1
	v_mov_b32_e32 v133, v163
	v_cvt_pk_fp8_f32 v133, v66, v70
	v_mul_f32_e32 v66, 0x43800000, v79
	v_mul_f32_e32 v70, 0x43800000, v87
	v_med3_f32 v66, v66, s19, v1
	v_med3_f32 v70, v70, s19, v1
	v_mov_b32_e32 v134, v163
	v_mul_f32_e32 v74, 0x43800000, v123
	v_mul_f32_e32 v78, 0x43800000, v127
	v_cvt_pk_fp8_f32 v134, v66, v70
	v_mul_f32_e32 v66, 0x43800000, v67
	v_mul_f32_e32 v67, 0x43800000, v71
	v_med3_f32 v74, v74, s19, v1
	v_med3_f32 v78, v78, s19, v1
	v_med3_f32 v66, v66, s19, v1
	v_med3_f32 v67, v67, s19, v1
	v_mov_b32_e32 v135, v163
	v_cvt_pk_fp8_f32 v132, v74, v78 op_sel:[0,0,1]
	v_mul_f32_e32 v74, 0x43800000, v107
	v_mul_f32_e32 v78, 0x43800000, v115
	v_cvt_pk_fp8_f32 v135, v66, v67
	v_med3_f32 v74, v74, s19, v1
	v_med3_f32 v78, v78, s19, v1
	v_cvt_pk_fp8_f32 v133, v74, v78 op_sel:[0,0,1]
	v_mul_f32_e32 v74, 0x43800000, v91
	v_mul_f32_e32 v78, 0x43800000, v99
	v_mul_f32_e32 v70, 0x43800000, v75
	v_mul_f32_e32 v71, 0x43800000, v83
	v_med3_f32 v74, v74, s19, v1
	v_med3_f32 v78, v78, s19, v1
	v_med3_f32 v70, v70, s19, v1
	v_med3_f32 v71, v71, s19, v1
	v_cvt_pk_fp8_f32 v134, v74, v78 op_sel:[0,0,1]
	v_cvt_pk_fp8_f32 v135, v70, v71 op_sel:[0,0,1]
	v_mul_f32_e32 v66, 0x43800000, v112
	v_mul_f32_e32 v67, 0x43800000, v120
	v_med3_f32 v66, v66, s19, v1
	ds_write_b128 v182, v[132:135] offset:272
	v_med3_f32 v67, v67, s19, v1
	v_mov_b32_e32 v132, v163
	v_cvt_pk_fp8_f32 v132, v66, v67
	v_mul_f32_e32 v66, 0x43800000, v96
	v_mul_f32_e32 v67, 0x43800000, v104
	v_med3_f32 v66, v66, s19, v1
	v_med3_f32 v67, v67, s19, v1
	v_mov_b32_e32 v133, v163
	v_mul_f32_e32 v70, 0x43800000, v124
	v_mul_f32_e32 v71, 0x43800000, v128
	v_cvt_pk_fp8_f32 v133, v66, v67
	v_mul_f32_e32 v66, 0x43800000, v80
	v_mul_f32_e32 v67, 0x43800000, v88
	v_med3_f32 v70, v70, s19, v1
	v_med3_f32 v71, v71, s19, v1
	v_med3_f32 v66, v66, s19, v1
	v_med3_f32 v67, v67, s19, v1
	v_mov_b32_e32 v134, v163
	v_cvt_pk_fp8_f32 v132, v70, v71 op_sel:[0,0,1]
	v_mul_f32_e32 v70, 0x43800000, v108
	v_mul_f32_e32 v71, 0x43800000, v116
	v_cvt_pk_fp8_f32 v134, v66, v67
	v_med3_f32 v70, v70, s19, v1
	v_med3_f32 v71, v71, s19, v1
	v_mul_f32_e32 v66, 0x43800000, v68
	v_mul_f32_e32 v67, 0x43800000, v72
	v_cvt_pk_fp8_f32 v133, v70, v71 op_sel:[0,0,1]
	v_mul_f32_e32 v70, 0x43800000, v92
	v_mul_f32_e32 v71, 0x43800000, v100
	v_med3_f32 v66, v66, s19, v1
	v_med3_f32 v67, v67, s19, v1
	v_mov_b32_e32 v135, v163
	v_med3_f32 v70, v70, s19, v1
	v_med3_f32 v71, v71, s19, v1
	v_cvt_pk_fp8_f32 v135, v66, v67
	v_mul_f32_e32 v66, 0x43800000, v113
	v_mul_f32_e32 v67, 0x43800000, v121
	v_cvt_pk_fp8_f32 v134, v70, v71 op_sel:[0,0,1]
	v_med3_f32 v71, v66, s19, v1
	v_med3_f32 v67, v67, s19, v1
	v_mov_b32_e32 v66, v163
	v_mul_f32_e32 v68, 0x43800000, v76
	v_mul_f32_e32 v70, 0x43800000, v84
	v_cvt_pk_fp8_f32 v66, v71, v67
	v_med3_f32 v68, v68, s19, v1
	v_med3_f32 v70, v70, s19, v1
	v_cvt_pk_fp8_f32 v135, v68, v70 op_sel:[0,0,1]
	v_mul_f32_e32 v68, 0x43800000, v125
	v_mul_f32_e32 v70, 0x43800000, v129
	v_med3_f32 v68, v68, s19, v1
	v_med3_f32 v70, v70, s19, v1
	v_cvt_pk_fp8_f32 v66, v68, v70 op_sel:[0,0,1]
	v_mul_f32_e32 v67, 0x43800000, v97
	v_mul_f32_e32 v68, 0x43800000, v105
	v_med3_f32 v72, v67, s19, v1
	v_med3_f32 v68, v68, s19, v1
	v_mov_b32_e32 v67, v163
	v_cvt_pk_fp8_f32 v67, v72, v68
	v_mul_f32_e32 v70, 0x43800000, v109
	v_mul_f32_e32 v71, 0x43800000, v117
	v_med3_f32 v70, v70, s19, v1
	v_med3_f32 v71, v71, s19, v1
	v_cvt_pk_fp8_f32 v67, v70, v71 op_sel:[0,0,1]
	v_mul_f32_e32 v68, 0x43800000, v81
	v_mul_f32_e32 v70, 0x43800000, v89
	v_med3_f32 v74, v68, s19, v1
	v_med3_f32 v70, v70, s19, v1
	v_mov_b32_e32 v68, v163
	v_cvt_pk_fp8_f32 v68, v74, v70
	v_mul_f32_e32 v69, 0x43800000, v69
	v_mul_f32_e32 v70, 0x43800000, v73
	v_med3_f32 v73, v69, s19, v1
	v_med3_f32 v70, v70, s19, v1
	v_mov_b32_e32 v69, v163
	v_mul_f32_e32 v71, 0x43800000, v93
	v_mul_f32_e32 v72, 0x43800000, v101
	v_cvt_pk_fp8_f32 v69, v73, v70
	v_med3_f32 v71, v71, s19, v1
	v_med3_f32 v72, v72, s19, v1
	v_cvt_pk_fp8_f32 v68, v71, v72 op_sel:[0,0,1]
	v_mul_f32_e32 v71, 0x43800000, v77
	v_mul_f32_e32 v72, 0x43800000, v85
	v_med3_f32 v71, v71, s19, v1
	v_med3_f32 v72, v72, s19, v1
	v_cvt_pk_fp8_f32 v69, v71, v72 op_sel:[0,0,1]
	ds_write_b128 v182, v[132:135] offset:544
	v_ashrrev_i32_e32 v132, 4, v130
	v_ashrrev_i32_e32 v133, 31, v132
	ds_write_b128 v182, v[66:69] offset:816
	v_lshlrev_b32_e32 v66, 4, v130
	v_and_b32_e32 v162, 0xf0, v66
	v_add_u32_e32 v66, 0x200, v130
	v_ashrrev_i32_e32 v136, 4, v66
	v_add_u32_e32 v66, 0x400, v130
	v_ashrrev_i32_e32 v140, 4, v66
	v_add_u32_e32 v66, 0x600, v130
	v_ashrrev_i32_e32 v144, 4, v66
	v_ashrrev_i32_e32 v137, 31, v136
	v_ashrrev_i32_e32 v141, 31, v140
	v_ashrrev_i32_e32 v145, 31, v144
	s_waitcnt lgkmcnt(0)
	s_barrier
	v_lshlrev_b64 v[134:135], 11, v[132:133]
	v_lshlrev_b64 v[138:139], 11, v[136:137]
	v_lshlrev_b64 v[142:143], 11, v[140:141]
	v_lshlrev_b64 v[146:147], 11, v[144:145]
	v_add_co_u32_e32 v66, vcc, s21, v180
	s_mov_b32 s2, 0x402000
	s_nop 0
	v_addc_co_u32_e32 v67, vcc, 0, v181, vcc
	v_add_co_u32_e32 v68, vcc, s2, v180
	s_mov_b32 s2, 0x406000
	s_nop 0
	v_addc_co_u32_e32 v69, vcc, 0, v181, vcc
	global_load_dwordx4 v[114:117], v[66:67], off sc0 nt
	global_load_dwordx4 v[122:125], v[68:69], off sc0 nt
	v_add_co_u32_e32 v66, vcc, s22, v180
	s_nop 1
	v_addc_co_u32_e32 v67, vcc, 0, v181, vcc
	v_add_co_u32_e32 v68, vcc, s2, v180
	s_mov_b32 s2, 0x40a000
	s_nop 0
	v_addc_co_u32_e32 v69, vcc, 0, v181, vcc
	global_load_dwordx4 v[126:129], v[66:67], off sc0 nt
	global_load_dwordx4 v[110:113], v[68:69], off sc0 nt
	v_add_co_u32_e32 v66, vcc, s23, v180
	s_nop 1
	v_addc_co_u32_e32 v67, vcc, 0, v181, vcc
	v_add_co_u32_e32 v68, vcc, s2, v180
	s_mov_b32 s2, 0x40e000
	s_nop 0
	v_addc_co_u32_e32 v69, vcc, 0, v181, vcc
	global_load_dwordx4 v[98:101], v[66:67], off sc0 nt
	global_load_dwordx4 v[106:109], v[68:69], off sc0 nt
	v_add_co_u32_e32 v66, vcc, s24, v180
	s_nop 1
	v_addc_co_u32_e32 v67, vcc, 0, v181, vcc
	v_add_co_u32_e32 v68, vcc, s2, v180
	s_mov_b32 s2, 0x412000
	s_nop 0
	v_addc_co_u32_e32 v69, vcc, 0, v181, vcc
	global_load_dwordx4 v[118:121], v[66:67], off sc0 nt
	global_load_dwordx4 v[94:97], v[68:69], off sc0 nt
	v_add_co_u32_e32 v66, vcc, s25, v180
	s_nop 1
	v_addc_co_u32_e32 v67, vcc, 0, v181, vcc
	v_add_co_u32_e32 v68, vcc, s2, v180
	s_mov_b32 s2, 0x416000
	s_nop 0
	v_addc_co_u32_e32 v69, vcc, 0, v181, vcc
	global_load_dwordx4 v[82:85], v[66:67], off sc0 nt
	global_load_dwordx4 v[90:93], v[68:69], off sc0 nt
	v_add_co_u32_e32 v66, vcc, s26, v180
	s_nop 1
	v_addc_co_u32_e32 v67, vcc, 0, v181, vcc
	v_add_co_u32_e32 v68, vcc, s2, v180
	s_mov_b32 s2, 0x41a000
	s_nop 0
	v_addc_co_u32_e32 v69, vcc, 0, v181, vcc
	global_load_dwordx4 v[102:105], v[66:67], off sc0 nt
	global_load_dwordx4 v[78:81], v[68:69], off sc0 nt
	v_add_co_u32_e32 v66, vcc, s27, v180
	s_nop 1
	v_addc_co_u32_e32 v67, vcc, 0, v181, vcc
	v_add_co_u32_e32 v68, vcc, s2, v180
	s_mov_b32 s2, 0x41e000
	s_nop 0
	v_addc_co_u32_e32 v69, vcc, 0, v181, vcc
	global_load_dwordx4 v[70:73], v[66:67], off sc0 nt
	global_load_dwordx4 v[74:77], v[68:69], off sc0 nt
	v_add_co_u32_e32 v66, vcc, s28, v180
	s_nop 1
	v_addc_co_u32_e32 v67, vcc, 0, v181, vcc
	v_add_co_u32_e32 v68, vcc, s2, v180
	s_nop 1
	v_addc_co_u32_e32 v69, vcc, 0, v181, vcc
	global_load_dwordx4 v[86:89], v[66:67], off sc0 nt
	s_nop 0
	global_load_dwordx4 v[66:69], v[68:69], off sc0 nt
	v_add_u32_e32 v148, 0, v162
	v_lshl_add_u64 v[150:151], s[10:11], 0, v[162:163]
	v_mad_u64_u32 v[168:169], s[10:11], v132, s20, v[148:149]
	ds_read_b128 v[130:133], v168
	v_lshl_add_u64 v[164:165], v[150:151], 0, v[134:135]
	v_mad_u64_u32 v[170:171], s[10:11], v136, s20, v[148:149]
	v_lshl_add_u64 v[166:167], v[150:151], 0, v[138:139]
	s_waitcnt lgkmcnt(0)
	global_store_dwordx4 v[164:165], v[130:133], off nt
	ds_read_b128 v[130:133], v170
	v_mad_u64_u32 v[174:175], s[10:11], v140, s20, v[148:149]
	v_lshl_add_u64 v[172:173], v[150:151], 0, v[142:143]
	v_mad_u64_u32 v[176:177], s[10:11], v144, s20, v[148:149]
	s_waitcnt lgkmcnt(0)
	global_store_dwordx4 v[166:167], v[130:133], off nt
	ds_read_b128 v[130:133], v174
	v_lshl_add_u64 v[178:179], v[150:151], 0, v[146:147]
	s_waitcnt lgkmcnt(0)
	global_store_dwordx4 v[172:173], v[130:133], off nt
	ds_read_b128 v[130:133], v176
	s_waitcnt lgkmcnt(0)
	global_store_dwordx4 v[178:179], v[130:133], off nt
	s_waitcnt vmcnt(35)
	v_mul_f32_e32 v50, 0x43800000, v50
	s_waitcnt vmcnt(34)
	v_mul_f32_e32 v54, 0x43800000, v54
	v_med3_f32 v50, v50, s19, v1
	v_med3_f32 v54, v54, s19, v1
	v_mov_b32_e32 v130, v163
	v_cvt_pk_fp8_f32 v130, v50, v54
	s_waitcnt vmcnt(31)
	v_mul_f32_e32 v34, 0x43800000, v34
	s_waitcnt vmcnt(30)
	v_mul_f32_e32 v38, 0x43800000, v38
	v_med3_f32 v34, v34, s19, v1
	v_med3_f32 v38, v38, s19, v1
	v_mov_b32_e32 v131, v163
	v_mul_f32_e32 v62, 0x43800000, v62
	v_mul_f32_e32 v42, 0x43800000, v42
	v_cvt_pk_fp8_f32 v131, v34, v38
	s_waitcnt vmcnt(27)
	v_mul_f32_e32 v18, 0x43800000, v18
	s_waitcnt vmcnt(26)
	v_mul_f32_e32 v22, 0x43800000, v22
	v_med3_f32 v50, v62, s19, v1
	v_med3_f32 v42, v42, s19, v1
	v_med3_f32 v18, v18, s19, v1
	v_med3_f32 v22, v22, s19, v1
	v_mov_b32_e32 v132, v163
	v_cvt_pk_fp8_f32 v130, v50, v42 op_sel:[0,0,1]
	v_mul_f32_e32 v42, 0x43800000, v58
	v_mul_f32_e32 v26, 0x43800000, v26
	v_cvt_pk_fp8_f32 v132, v18, v22
	s_waitcnt vmcnt(23)
	v_mul_f32_e32 v6, 0x43800000, v6
	s_waitcnt vmcnt(22)
	v_mul_f32_e32 v10, 0x43800000, v10
	v_med3_f32 v34, v42, s19, v1
	v_med3_f32 v26, v26, s19, v1
	v_med3_f32 v6, v6, s19, v1
	v_med3_f32 v10, v10, s19, v1
	v_mov_b32_e32 v133, v163
	v_cvt_pk_fp8_f32 v131, v34, v26 op_sel:[0,0,1]
	v_mul_f32_e32 v26, 0x43800000, v46
	v_mul_f32_e32 v14, 0x43800000, v14
	v_cvt_pk_fp8_f32 v133, v6, v10
	v_med3_f32 v18, v26, s19, v1
	v_med3_f32 v14, v14, s19, v1
	v_cvt_pk_fp8_f32 v132, v18, v14 op_sel:[0,0,1]
	s_waitcnt vmcnt(21)
	v_mul_f32_e32 v14, 0x43800000, v30
	s_waitcnt vmcnt(20)
	v_mul_f32_e32 v2, 0x43800000, v2
	v_med3_f32 v6, v14, s19, v1
	v_med3_f32 v2, v2, s19, v1
	v_cvt_pk_fp8_f32 v133, v6, v2 op_sel:[0,0,1]
	v_mul_f32_e32 v2, 0x43800000, v51
	v_mul_f32_e32 v6, 0x43800000, v55
	v_med3_f32 v2, v2, s19, v1
	v_med3_f32 v6, v6, s19, v1
	v_mov_b32_e32 v134, v163
	v_cvt_pk_fp8_f32 v134, v2, v6
	v_mul_f32_e32 v10, 0x43800000, v63
	v_mul_f32_e32 v2, 0x43800000, v43
	v_med3_f32 v6, v10, s19, v1
	v_med3_f32 v2, v2, s19, v1
	v_cvt_pk_fp8_f32 v134, v6, v2 op_sel:[0,0,1]
	v_mul_f32_e32 v2, 0x43800000, v35
	v_mul_f32_e32 v6, 0x43800000, v39
	v_med3_f32 v2, v2, s19, v1
	v_med3_f32 v6, v6, s19, v1
	v_mov_b32_e32 v135, v163
	v_cvt_pk_fp8_f32 v135, v2, v6
	v_mul_f32_e32 v10, 0x43800000, v59
	v_mul_f32_e32 v2, 0x43800000, v27
	v_med3_f32 v6, v10, s19, v1
	v_med3_f32 v2, v2, s19, v1
	v_cvt_pk_fp8_f32 v135, v6, v2 op_sel:[0,0,1]
	v_mul_f32_e32 v2, 0x43800000, v19
	v_mul_f32_e32 v6, 0x43800000, v23
	v_med3_f32 v2, v2, s19, v1
	v_med3_f32 v6, v6, s19, v1
	v_mov_b32_e32 v136, v163
	v_cvt_pk_fp8_f32 v136, v2, v6
	v_mul_f32_e32 v10, 0x43800000, v47
	v_mul_f32_e32 v2, 0x43800000, v15
	v_med3_f32 v6, v10, s19, v1
	v_med3_f32 v2, v2, s19, v1
	v_cvt_pk_fp8_f32 v136, v6, v2 op_sel:[0,0,1]
	v_mul_f32_e32 v2, 0x43800000, v7
	v_mul_f32_e32 v6, 0x43800000, v11
	v_med3_f32 v2, v2, s19, v1
	v_med3_f32 v6, v6, s19, v1
	v_mov_b32_e32 v137, v163
	v_cvt_pk_fp8_f32 v137, v2, v6
	v_mul_f32_e32 v7, 0x43800000, v31
	v_mul_f32_e32 v2, 0x43800000, v3
	v_med3_f32 v3, v7, s19, v1
	v_med3_f32 v2, v2, s19, v1
	v_cvt_pk_fp8_f32 v137, v3, v2 op_sel:[0,0,1]
	v_mul_f32_e32 v2, 0x43800000, v52
	v_mul_f32_e32 v3, 0x43800000, v56
	v_med3_f32 v2, v2, s19, v1
	v_med3_f32 v3, v3, s19, v1
	v_mov_b32_e32 v138, v163
	v_cvt_pk_fp8_f32 v138, v2, v3
	v_mul_f32_e32 v6, 0x43800000, v64
	v_mul_f32_e32 v2, 0x43800000, v44
	v_med3_f32 v3, v6, s19, v1
	v_med3_f32 v2, v2, s19, v1
	v_cvt_pk_fp8_f32 v138, v3, v2 op_sel:[0,0,1]
	v_mul_f32_e32 v2, 0x43800000, v36
	v_mul_f32_e32 v3, 0x43800000, v40
	v_med3_f32 v2, v2, s19, v1
	v_med3_f32 v3, v3, s19, v1
	v_mov_b32_e32 v139, v163
	v_cvt_pk_fp8_f32 v139, v2, v3
	v_mul_f32_e32 v6, 0x43800000, v60
	v_mul_f32_e32 v2, 0x43800000, v28
	v_med3_f32 v3, v6, s19, v1
	v_med3_f32 v2, v2, s19, v1
	v_cvt_pk_fp8_f32 v139, v3, v2 op_sel:[0,0,1]
	v_mul_f32_e32 v2, 0x43800000, v20
	v_mul_f32_e32 v3, 0x43800000, v24
	v_med3_f32 v2, v2, s19, v1
	v_med3_f32 v3, v3, s19, v1
	v_mov_b32_e32 v140, v163
	v_cvt_pk_fp8_f32 v140, v2, v3
	v_mul_f32_e32 v6, 0x43800000, v48
	v_mul_f32_e32 v2, 0x43800000, v16
	v_med3_f32 v3, v6, s19, v1
	v_med3_f32 v2, v2, s19, v1
	v_cvt_pk_fp8_f32 v140, v3, v2 op_sel:[0,0,1]
	v_mul_f32_e32 v2, 0x43800000, v8
	v_mul_f32_e32 v3, 0x43800000, v12
	v_med3_f32 v2, v2, s19, v1
	v_med3_f32 v3, v3, s19, v1
	v_mov_b32_e32 v141, v163
	v_cvt_pk_fp8_f32 v141, v2, v3
	v_mul_f32_e32 v6, 0x43800000, v32
	v_mul_f32_e32 v2, 0x43800000, v4
	v_med3_f32 v3, v6, s19, v1
	v_med3_f32 v2, v2, s19, v1
	v_cvt_pk_fp8_f32 v141, v3, v2 op_sel:[0,0,1]
	v_mul_f32_e32 v2, 0x43800000, v53
	v_mul_f32_e32 v3, 0x43800000, v57
	v_med3_f32 v2, v2, s19, v1
	v_med3_f32 v3, v3, s19, v1
	v_mov_b32_e32 v6, v163
	v_cvt_pk_fp8_f32 v6, v2, v3
	v_mul_f32_e32 v4, 0x43800000, v65
	v_mul_f32_e32 v2, 0x43800000, v45
	v_med3_f32 v3, v4, s19, v1
	v_med3_f32 v2, v2, s19, v1
	v_cvt_pk_fp8_f32 v6, v3, v2 op_sel:[0,0,1]
	v_mul_f32_e32 v2, 0x43800000, v37
	v_mul_f32_e32 v3, 0x43800000, v41
	v_med3_f32 v2, v2, s19, v1
	v_med3_f32 v3, v3, s19, v1
	v_mov_b32_e32 v7, v163
	v_cvt_pk_fp8_f32 v7, v2, v3
	v_mul_f32_e32 v4, 0x43800000, v61
	v_mul_f32_e32 v2, 0x43800000, v29
	v_med3_f32 v3, v4, s19, v1
	v_med3_f32 v2, v2, s19, v1
	v_cvt_pk_fp8_f32 v7, v3, v2 op_sel:[0,0,1]
	v_mul_f32_e32 v2, 0x43800000, v21
	v_mul_f32_e32 v3, 0x43800000, v25
	v_med3_f32 v2, v2, s19, v1
	v_med3_f32 v3, v3, s19, v1
	v_mov_b32_e32 v8, v163
	v_cvt_pk_fp8_f32 v8, v2, v3
	v_mul_f32_e32 v4, 0x43800000, v49
	v_mul_f32_e32 v2, 0x43800000, v17
	v_med3_f32 v3, v4, s19, v1
	v_med3_f32 v2, v2, s19, v1
	v_cvt_pk_fp8_f32 v8, v3, v2 op_sel:[0,0,1]
	v_mul_f32_e32 v2, 0x43800000, v9
	v_mul_f32_e32 v3, 0x43800000, v13
	v_med3_f32 v2, v2, s19, v1
	v_med3_f32 v3, v3, s19, v1
	v_mov_b32_e32 v9, v163
	v_cvt_pk_fp8_f32 v9, v2, v3
	v_mul_f32_e32 v4, 0x43800000, v33
	v_mul_f32_e32 v2, 0x43800000, v5
	v_med3_f32 v3, v4, s19, v1
	v_med3_f32 v2, v2, s19, v1
	v_cvt_pk_fp8_f32 v9, v3, v2 op_sel:[0,0,1]
	ds_write_b128 v182, v[130:133] offset:34816
	ds_write_b128 v182, v[134:137] offset:35088
	ds_write_b128 v182, v[138:141] offset:35360
	ds_write_b128 v182, v[6:9] offset:35632
	s_waitcnt lgkmcnt(0)
	s_barrier
	s_mov_b32 s2, 0x600000
	v_add_co_u32_e32 v2, vcc, s2, v180
	s_mov_b32 s2, 0x602000
	s_nop 0
	v_addc_co_u32_e32 v3, vcc, 0, v181, vcc
	v_add_co_u32_e32 v4, vcc, s2, v180
	s_mov_b32 s2, 0x604000
	s_nop 0
	v_addc_co_u32_e32 v5, vcc, 0, v181, vcc
	global_load_dwordx4 v[146:149], v[2:3], off sc0 nt
	global_load_dwordx4 v[150:153], v[4:5], off sc0 nt
	v_add_co_u32_e32 v2, vcc, s2, v180
	s_mov_b32 s2, 0x606000
	s_nop 0
	v_addc_co_u32_e32 v3, vcc, 0, v181, vcc
	v_add_co_u32_e32 v4, vcc, s2, v180
	s_mov_b32 s2, 0x608000
	s_nop 0
	v_addc_co_u32_e32 v5, vcc, 0, v181, vcc
	global_load_dwordx4 v[158:161], v[2:3], off sc0 nt
	global_load_dwordx4 v[138:141], v[4:5], off sc0 nt
	v_add_co_u32_e32 v2, vcc, s2, v180
	s_mov_b32 s2, 0x60a000
	s_nop 0
	v_addc_co_u32_e32 v3, vcc, 0, v181, vcc
	v_add_co_u32_e32 v4, vcc, s2, v180
	s_mov_b32 s2, 0x60c000
	s_nop 0
	v_addc_co_u32_e32 v5, vcc, 0, v181, vcc
	global_load_dwordx4 v[130:133], v[2:3], off sc0 nt
	global_load_dwordx4 v[134:137], v[4:5], off sc0 nt
	v_add_co_u32_e32 v2, vcc, s2, v180
	s_mov_b32 s2, 0x60e000
	s_nop 0
	v_addc_co_u32_e32 v3, vcc, 0, v181, vcc
	v_add_co_u32_e32 v4, vcc, s2, v180
	s_mov_b32 s2, 0x610000
	s_nop 0
	v_addc_co_u32_e32 v5, vcc, 0, v181, vcc
	global_load_dwordx4 v[154:157], v[2:3], off sc0 nt
	global_load_dwordx4 v[58:61], v[4:5], off sc0 nt
	v_add_co_u32_e32 v2, vcc, s2, v180
	s_mov_b32 s2, 0x612000
	s_nop 0
	v_addc_co_u32_e32 v3, vcc, 0, v181, vcc
	v_add_co_u32_e32 v4, vcc, s2, v180
	s_mov_b32 s2, 0x614000
	s_nop 0
	v_addc_co_u32_e32 v5, vcc, 0, v181, vcc
	global_load_dwordx4 v[46:49], v[2:3], off sc0 nt
	global_load_dwordx4 v[54:57], v[4:5], off sc0 nt
	v_add_co_u32_e32 v2, vcc, s2, v180
	s_mov_b32 s2, 0x616000
	s_nop 0
	v_addc_co_u32_e32 v3, vcc, 0, v181, vcc
	v_add_co_u32_e32 v4, vcc, s2, v180
	s_mov_b32 s2, 0x618000
	s_nop 0
	v_addc_co_u32_e32 v5, vcc, 0, v181, vcc
	global_load_dwordx4 v[142:145], v[2:3], off sc0 nt
	global_load_dwordx4 v[38:41], v[4:5], off sc0 nt
	v_add_co_u32_e32 v2, vcc, s2, v180
	s_mov_b32 s2, 0x61a000
	s_nop 0
	v_addc_co_u32_e32 v3, vcc, 0, v181, vcc
	v_add_co_u32_e32 v4, vcc, s2, v180
	s_mov_b32 s2, 0x61c000
	s_nop 0
	v_addc_co_u32_e32 v5, vcc, 0, v181, vcc
	global_load_dwordx4 v[22:25], v[2:3], off sc0 nt
	global_load_dwordx4 v[26:29], v[4:5], off sc0 nt
	v_add_co_u32_e32 v2, vcc, s2, v180
	s_mov_b32 s2, 0x61e000
	s_nop 0
	v_addc_co_u32_e32 v3, vcc, 0, v181, vcc
	v_add_co_u32_e32 v4, vcc, s2, v180
	s_nop 1
	v_addc_co_u32_e32 v5, vcc, 0, v181, vcc
	global_load_dwordx4 v[62:65], v[2:3], off sc0 nt
	global_load_dwordx4 v[14:17], v[4:5], off sc0 nt
	ds_read_b128 v[2:5], v168 offset:34816
	ds_read_b128 v[6:9], v170 offset:34816
	ds_read_b128 v[10:13], v174 offset:34816
	ds_read_b128 v[18:21], v176 offset:34816
	s_waitcnt lgkmcnt(3)
	global_store_dwordx4 v[164:165], v[2:5], off offset:256 nt
	s_waitcnt lgkmcnt(2)
	global_store_dwordx4 v[166:167], v[6:9], off offset:256 nt
	s_waitcnt lgkmcnt(1)
	global_store_dwordx4 v[172:173], v[10:13], off offset:256 nt
	s_waitcnt lgkmcnt(0)
	global_store_dwordx4 v[178:179], v[18:21], off offset:256 nt
	s_waitcnt vmcnt(39)
	v_mul_f32_e32 v2, 0x43800000, v114
	s_waitcnt vmcnt(38)
	v_mul_f32_e32 v3, 0x43800000, v122
	v_med3_f32 v5, v2, s19, v1
	v_med3_f32 v3, v3, s19, v1
	v_mov_b32_e32 v2, v163
	v_cvt_pk_fp8_f32 v2, v5, v3
	s_waitcnt vmcnt(37)
	v_mul_f32_e32 v4, 0x43800000, v126
	s_waitcnt vmcnt(36)
	v_mul_f32_e32 v3, 0x43800000, v110
	v_med3_f32 v4, v4, s19, v1
	v_med3_f32 v3, v3, s19, v1
	v_cvt_pk_fp8_f32 v2, v4, v3 op_sel:[0,0,1]
	s_waitcnt vmcnt(35)
	v_mul_f32_e32 v3, 0x43800000, v98
	s_waitcnt vmcnt(34)
	v_mul_f32_e32 v4, 0x43800000, v106
	v_med3_f32 v6, v3, s19, v1
	v_med3_f32 v4, v4, s19, v1
	v_mov_b32_e32 v3, v163
	v_cvt_pk_fp8_f32 v3, v6, v4
	s_waitcnt vmcnt(33)
	v_mul_f32_e32 v5, 0x43800000, v118
	s_waitcnt vmcnt(32)
	v_mul_f32_e32 v4, 0x43800000, v94
	v_med3_f32 v5, v5, s19, v1
	v_med3_f32 v4, v4, s19, v1
	v_cvt_pk_fp8_f32 v3, v5, v4 op_sel:[0,0,1]
	s_waitcnt vmcnt(31)
	v_mul_f32_e32 v4, 0x43800000, v82
	s_waitcnt vmcnt(30)
	v_mul_f32_e32 v5, 0x43800000, v90
	v_med3_f32 v7, v4, s19, v1
	v_med3_f32 v5, v5, s19, v1
	v_mov_b32_e32 v4, v163
	v_cvt_pk_fp8_f32 v4, v7, v5
	s_waitcnt vmcnt(29)
	v_mul_f32_e32 v6, 0x43800000, v102
	s_waitcnt vmcnt(28)
	v_mul_f32_e32 v5, 0x43800000, v78
	v_med3_f32 v6, v6, s19, v1
	v_med3_f32 v5, v5, s19, v1
	v_cvt_pk_fp8_f32 v4, v6, v5 op_sel:[0,0,1]
	s_waitcnt vmcnt(27)
	v_mul_f32_e32 v5, 0x43800000, v70
	s_waitcnt vmcnt(26)
	v_mul_f32_e32 v6, 0x43800000, v74
	v_med3_f32 v8, v5, s19, v1
	v_med3_f32 v6, v6, s19, v1
	v_mov_b32_e32 v5, v163
	v_cvt_pk_fp8_f32 v5, v8, v6
	s_waitcnt vmcnt(25)
	v_mul_f32_e32 v7, 0x43800000, v86
	s_waitcnt vmcnt(24)
	v_mul_f32_e32 v6, 0x43800000, v66
	v_med3_f32 v7, v7, s19, v1
	v_med3_f32 v6, v6, s19, v1
	v_cvt_pk_fp8_f32 v5, v7, v6 op_sel:[0,0,1]
	v_mul_f32_e32 v6, 0x43800000, v115
	v_mul_f32_e32 v7, 0x43800000, v123
	v_med3_f32 v9, v6, s19, v1
	v_med3_f32 v7, v7, s19, v1
	v_mov_b32_e32 v6, v163
	v_cvt_pk_fp8_f32 v6, v9, v7
	v_mul_f32_e32 v8, 0x43800000, v127
	v_mul_f32_e32 v7, 0x43800000, v111
	v_med3_f32 v8, v8, s19, v1
	v_med3_f32 v7, v7, s19, v1
	v_cvt_pk_fp8_f32 v6, v8, v7 op_sel:[0,0,1]
	v_mul_f32_e32 v7, 0x43800000, v99
	v_mul_f32_e32 v8, 0x43800000, v107
	v_med3_f32 v10, v7, s19, v1
	v_med3_f32 v8, v8, s19, v1
	v_mov_b32_e32 v7, v163
	v_cvt_pk_fp8_f32 v7, v10, v8
	v_mul_f32_e32 v9, 0x43800000, v119
	v_mul_f32_e32 v8, 0x43800000, v95
	v_med3_f32 v9, v9, s19, v1
	v_med3_f32 v8, v8, s19, v1
	v_cvt_pk_fp8_f32 v7, v9, v8 op_sel:[0,0,1]
	v_mul_f32_e32 v8, 0x43800000, v83
	v_mul_f32_e32 v9, 0x43800000, v91
	v_med3_f32 v11, v8, s19, v1
	v_med3_f32 v9, v9, s19, v1
	v_mov_b32_e32 v8, v163
	v_cvt_pk_fp8_f32 v8, v11, v9
	v_mul_f32_e32 v10, 0x43800000, v103
	v_mul_f32_e32 v9, 0x43800000, v79
	v_med3_f32 v10, v10, s19, v1
	v_med3_f32 v9, v9, s19, v1
	v_cvt_pk_fp8_f32 v8, v10, v9 op_sel:[0,0,1]
	v_mul_f32_e32 v9, 0x43800000, v71
	v_mul_f32_e32 v10, 0x43800000, v75
	v_med3_f32 v12, v9, s19, v1
	v_med3_f32 v10, v10, s19, v1
	v_mov_b32_e32 v9, v163
	v_cvt_pk_fp8_f32 v9, v12, v10
	v_mul_f32_e32 v11, 0x43800000, v87
	v_mul_f32_e32 v10, 0x43800000, v67
	v_med3_f32 v11, v11, s19, v1
	v_med3_f32 v10, v10, s19, v1
	v_cvt_pk_fp8_f32 v9, v11, v10 op_sel:[0,0,1]
	v_mul_f32_e32 v10, 0x43800000, v116
	v_mul_f32_e32 v11, 0x43800000, v124
	v_med3_f32 v13, v10, s19, v1
	v_med3_f32 v11, v11, s19, v1
	v_mov_b32_e32 v10, v163
	v_cvt_pk_fp8_f32 v10, v13, v11
	v_mul_f32_e32 v12, 0x43800000, v128
	v_mul_f32_e32 v11, 0x43800000, v112
	v_med3_f32 v12, v12, s19, v1
	v_med3_f32 v11, v11, s19, v1
	v_cvt_pk_fp8_f32 v10, v12, v11 op_sel:[0,0,1]
	v_mul_f32_e32 v11, 0x43800000, v100
	v_mul_f32_e32 v12, 0x43800000, v108
	v_med3_f32 v18, v11, s19, v1
	v_med3_f32 v12, v12, s19, v1
	v_mov_b32_e32 v11, v163
	v_cvt_pk_fp8_f32 v11, v18, v12
	v_mul_f32_e32 v13, 0x43800000, v120
	v_mul_f32_e32 v12, 0x43800000, v96
	v_med3_f32 v13, v13, s19, v1
	v_med3_f32 v12, v12, s19, v1
	v_cvt_pk_fp8_f32 v11, v13, v12 op_sel:[0,0,1]
	v_mul_f32_e32 v12, 0x43800000, v84
	v_mul_f32_e32 v13, 0x43800000, v92
	v_med3_f32 v19, v12, s19, v1
	v_med3_f32 v13, v13, s19, v1
	v_mov_b32_e32 v12, v163
	v_cvt_pk_fp8_f32 v12, v19, v13
	v_mul_f32_e32 v18, 0x43800000, v104
	v_mul_f32_e32 v13, 0x43800000, v80
	v_med3_f32 v18, v18, s19, v1
	v_med3_f32 v13, v13, s19, v1
	v_cvt_pk_fp8_f32 v12, v18, v13 op_sel:[0,0,1]
	v_mul_f32_e32 v13, 0x43800000, v72
	v_mul_f32_e32 v18, 0x43800000, v76
	v_med3_f32 v20, v13, s19, v1
	v_med3_f32 v18, v18, s19, v1
	v_mov_b32_e32 v13, v163
	v_cvt_pk_fp8_f32 v13, v20, v18
	v_mul_f32_e32 v19, 0x43800000, v88
	v_mul_f32_e32 v18, 0x43800000, v68
	v_med3_f32 v19, v19, s19, v1
	v_med3_f32 v18, v18, s19, v1
	v_cvt_pk_fp8_f32 v13, v19, v18 op_sel:[0,0,1]
	v_mul_f32_e32 v18, 0x43800000, v117
	v_mul_f32_e32 v19, 0x43800000, v125
	v_med3_f32 v21, v18, s19, v1
	v_med3_f32 v19, v19, s19, v1
	v_mov_b32_e32 v18, v163
	v_cvt_pk_fp8_f32 v18, v21, v19
	v_mul_f32_e32 v20, 0x43800000, v129
	v_mul_f32_e32 v19, 0x43800000, v113
	v_med3_f32 v20, v20, s19, v1
	v_med3_f32 v19, v19, s19, v1
	v_cvt_pk_fp8_f32 v18, v20, v19 op_sel:[0,0,1]
	v_mul_f32_e32 v19, 0x43800000, v101
	v_mul_f32_e32 v20, 0x43800000, v109
	v_med3_f32 v30, v19, s19, v1
	v_med3_f32 v20, v20, s19, v1
	v_mov_b32_e32 v19, v163
	v_cvt_pk_fp8_f32 v19, v30, v20
	v_mul_f32_e32 v21, 0x43800000, v121
	v_mul_f32_e32 v20, 0x43800000, v97
	v_med3_f32 v21, v21, s19, v1
	v_med3_f32 v20, v20, s19, v1
	v_cvt_pk_fp8_f32 v19, v21, v20 op_sel:[0,0,1]
	v_mul_f32_e32 v20, 0x43800000, v85
	v_mul_f32_e32 v21, 0x43800000, v93
	v_med3_f32 v31, v20, s19, v1
	v_med3_f32 v21, v21, s19, v1
	v_mov_b32_e32 v20, v163
	v_cvt_pk_fp8_f32 v20, v31, v21
	v_mul_f32_e32 v30, 0x43800000, v105
	v_mul_f32_e32 v21, 0x43800000, v81
	v_med3_f32 v30, v30, s19, v1
	v_med3_f32 v21, v21, s19, v1
	v_cvt_pk_fp8_f32 v20, v30, v21 op_sel:[0,0,1]
	v_mul_f32_e32 v21, 0x43800000, v73
	v_mul_f32_e32 v30, 0x43800000, v77
	v_med3_f32 v32, v21, s19, v1
	v_med3_f32 v30, v30, s19, v1
	v_mov_b32_e32 v21, v163
	v_cvt_pk_fp8_f32 v21, v32, v30
	v_mul_f32_e32 v31, 0x43800000, v89
	v_mul_f32_e32 v30, 0x43800000, v69
	v_med3_f32 v31, v31, s19, v1
	v_med3_f32 v30, v30, s19, v1
	v_cvt_pk_fp8_f32 v21, v31, v30 op_sel:[0,0,1]
	ds_write_b128 v182, v[2:5]
	ds_write_b128 v182, v[6:9] offset:272
	ds_write_b128 v182, v[10:13] offset:544
	ds_write_b128 v182, v[18:21] offset:816
	s_waitcnt lgkmcnt(0)
	s_barrier
	v_add_co_u32_e32 v2, vcc, s29, v180
	s_mov_b32 s2, 0x802000
	s_nop 0
	v_addc_co_u32_e32 v3, vcc, 0, v181, vcc
	v_add_co_u32_e32 v4, vcc, s2, v180
	s_mov_b32 s2, 0x806000
	s_nop 0
	v_addc_co_u32_e32 v5, vcc, 0, v181, vcc
	global_load_dwordx4 v[98:101], v[2:3], off sc0 nt
	global_load_dwordx4 v[110:113], v[4:5], off sc0 nt
	v_add_co_u32_e32 v2, vcc, s30, v180
	s_nop 1
	v_addc_co_u32_e32 v3, vcc, 0, v181, vcc
	v_add_co_u32_e32 v4, vcc, s2, v180
	s_mov_b32 s2, 0x80a000
	s_nop 0
	v_addc_co_u32_e32 v5, vcc, 0, v181, vcc
	global_load_dwordx4 v[122:125], v[2:3], off sc0 nt
	global_load_dwordx4 v[82:85], v[4:5], off sc0 nt
	v_add_co_u32_e32 v2, vcc, s31, v180
	s_nop 1
	v_addc_co_u32_e32 v3, vcc, 0, v181, vcc
	v_add_co_u32_e32 v4, vcc, s2, v180
	s_mov_b32 s2, 0x80e000
	s_nop 0
	v_addc_co_u32_e32 v5, vcc, 0, v181, vcc
	global_load_dwordx4 v[66:69], v[2:3], off sc0 nt
	global_load_dwordx4 v[74:77], v[4:5], off sc0 nt
	v_add_co_u32_e32 v2, vcc, s33, v180
	s_nop 1
	v_addc_co_u32_e32 v3, vcc, 0, v181, vcc
	v_add_co_u32_e32 v4, vcc, s2, v180
	s_mov_b32 s2, 0x812000
	s_nop 0
	v_addc_co_u32_e32 v5, vcc, 0, v181, vcc
	global_load_dwordx4 v[102:105], v[2:3], off sc0 nt
	global_load_dwordx4 v[50:53], v[4:5], off sc0 nt
	v_add_co_u32_e32 v2, vcc, s50, v180
	s_nop 1
	v_addc_co_u32_e32 v3, vcc, 0, v181, vcc
	v_add_co_u32_e32 v4, vcc, s2, v180
	s_mov_b32 s2, 0x816000
	s_nop 0
	v_addc_co_u32_e32 v5, vcc, 0, v181, vcc
	global_load_dwordx4 v[30:33], v[2:3], off sc0 nt
	global_load_dwordx4 v[42:45], v[4:5], off sc0 nt
	v_add_co_u32_e32 v2, vcc, s51, v180
	s_nop 1
	v_addc_co_u32_e32 v3, vcc, 0, v181, vcc
	v_add_co_u32_e32 v4, vcc, s2, v180
	s_mov_b32 s2, 0x81a000
	s_nop 0
	v_addc_co_u32_e32 v5, vcc, 0, v181, vcc
	global_load_dwordx4 v[70:73], v[2:3], off sc0 nt
	global_load_dwordx4 v[18:21], v[4:5], off sc0 nt
	v_add_co_u32_e32 v2, vcc, s54, v180
	s_nop 1
	v_addc_co_u32_e32 v3, vcc, 0, v181, vcc
	v_add_co_u32_e32 v4, vcc, s2, v180
	s_mov_b32 s2, 0x81e000
	s_nop 0
	v_addc_co_u32_e32 v5, vcc, 0, v181, vcc
	global_load_dwordx4 v[6:9], v[2:3], off sc0 nt
	global_load_dwordx4 v[10:13], v[4:5], off sc0 nt
	v_add_co_u32_e32 v2, vcc, s55, v180
	s_nop 1
	v_addc_co_u32_e32 v3, vcc, 0, v181, vcc
	v_add_co_u32_e32 v4, vcc, s2, v180
	s_nop 1
	v_addc_co_u32_e32 v5, vcc, 0, v181, vcc
	global_load_dwordx4 v[34:37], v[2:3], off sc0 nt
	s_nop 0
	global_load_dwordx4 v[2:5], v[4:5], off sc0 nt
	ds_read_b128 v[78:81], v168
	ds_read_b128 v[86:89], v170
	ds_read_b128 v[90:93], v174
	ds_read_b128 v[94:97], v176
	s_waitcnt lgkmcnt(3)
	global_store_dwordx4 v[164:165], v[78:81], off offset:512 nt
	s_waitcnt lgkmcnt(2)
	global_store_dwordx4 v[166:167], v[86:89], off offset:512 nt
	s_waitcnt lgkmcnt(1)
	global_store_dwordx4 v[172:173], v[90:93], off offset:512 nt
	s_waitcnt lgkmcnt(0)
	global_store_dwordx4 v[178:179], v[94:97], off offset:512 nt
	s_waitcnt vmcnt(39)
	v_mul_f32_e32 v78, 0x43800000, v146
	s_waitcnt vmcnt(38)
	v_mul_f32_e32 v79, 0x43800000, v150
	v_med3_f32 v81, v78, s19, v1
	v_med3_f32 v79, v79, s19, v1
	v_mov_b32_e32 v78, v163
	v_cvt_pk_fp8_f32 v78, v81, v79
	s_waitcnt vmcnt(37)
	v_mul_f32_e32 v80, 0x43800000, v158
	s_waitcnt vmcnt(36)
	v_mul_f32_e32 v79, 0x43800000, v138
	v_med3_f32 v80, v80, s19, v1
	v_med3_f32 v79, v79, s19, v1
	v_cvt_pk_fp8_f32 v78, v80, v79 op_sel:[0,0,1]
	s_waitcnt vmcnt(35)
	v_mul_f32_e32 v79, 0x43800000, v130
	s_waitcnt vmcnt(34)
	v_mul_f32_e32 v80, 0x43800000, v134
	v_med3_f32 v86, v79, s19, v1
	v_med3_f32 v80, v80, s19, v1
	v_mov_b32_e32 v79, v163
	v_cvt_pk_fp8_f32 v79, v86, v80
	s_waitcnt vmcnt(33)
	v_mul_f32_e32 v81, 0x43800000, v154
	s_waitcnt vmcnt(32)
	v_mul_f32_e32 v58, 0x43800000, v58
	v_med3_f32 v80, v81, s19, v1
	v_med3_f32 v58, v58, s19, v1
	s_waitcnt vmcnt(31)
	v_mul_f32_e32 v46, 0x43800000, v46
	s_waitcnt vmcnt(30)
	v_mul_f32_e32 v54, 0x43800000, v54
	v_cvt_pk_fp8_f32 v79, v80, v58 op_sel:[0,0,1]
	v_med3_f32 v46, v46, s19, v1
	v_med3_f32 v54, v54, s19, v1
	v_mov_b32_e32 v80, v163
	v_cvt_pk_fp8_f32 v80, v46, v54
	s_waitcnt vmcnt(27)
	v_mul_f32_e32 v22, 0x43800000, v22
	s_waitcnt vmcnt(26)
	v_mul_f32_e32 v26, 0x43800000, v26
	v_med3_f32 v22, v22, s19, v1
	v_med3_f32 v26, v26, s19, v1
	v_mov_b32_e32 v81, v163
	v_mul_f32_e32 v58, 0x43800000, v142
	v_mul_f32_e32 v38, 0x43800000, v38
	v_cvt_pk_fp8_f32 v81, v22, v26
	v_med3_f32 v46, v58, s19, v1
	v_med3_f32 v38, v38, s19, v1
	v_cvt_pk_fp8_f32 v80, v46, v38 op_sel:[0,0,1]
	s_waitcnt vmcnt(25)
	v_mul_f32_e32 v38, 0x43800000, v62
	s_waitcnt vmcnt(24)
	v_mul_f32_e32 v14, 0x43800000, v14
	v_med3_f32 v22, v38, s19, v1
	v_med3_f32 v14, v14, s19, v1
	v_cvt_pk_fp8_f32 v81, v22, v14 op_sel:[0,0,1]
	v_mul_f32_e32 v14, 0x43800000, v147
	v_mul_f32_e32 v22, 0x43800000, v151
	v_med3_f32 v14, v14, s19, v1
	v_med3_f32 v22, v22, s19, v1
	v_mov_b32_e32 v86, v163
	v_cvt_pk_fp8_f32 v86, v14, v22
	v_mul_f32_e32 v26, 0x43800000, v159
	v_mul_f32_e32 v14, 0x43800000, v139
	v_med3_f32 v22, v26, s19, v1
	v_med3_f32 v14, v14, s19, v1
	v_cvt_pk_fp8_f32 v86, v22, v14 op_sel:[0,0,1]
	v_mul_f32_e32 v14, 0x43800000, v131
	v_mul_f32_e32 v22, 0x43800000, v135
	v_med3_f32 v14, v14, s19, v1
	v_med3_f32 v22, v22, s19, v1
	v_mov_b32_e32 v87, v163
	v_cvt_pk_fp8_f32 v87, v14, v22
	v_mul_f32_e32 v26, 0x43800000, v155
	v_mul_f32_e32 v14, 0x43800000, v59
	v_med3_f32 v22, v26, s19, v1
	v_med3_f32 v14, v14, s19, v1
	v_cvt_pk_fp8_f32 v87, v22, v14 op_sel:[0,0,1]
	v_mul_f32_e32 v14, 0x43800000, v47
	v_mul_f32_e32 v22, 0x43800000, v55
	v_med3_f32 v14, v14, s19, v1
	v_med3_f32 v22, v22, s19, v1
	v_mov_b32_e32 v88, v163
	v_cvt_pk_fp8_f32 v88, v14, v22
	v_mul_f32_e32 v26, 0x43800000, v143
	v_mul_f32_e32 v14, 0x43800000, v39
	v_med3_f32 v22, v26, s19, v1
	v_med3_f32 v14, v14, s19, v1
	v_cvt_pk_fp8_f32 v88, v22, v14 op_sel:[0,0,1]
	v_mul_f32_e32 v14, 0x43800000, v23
	v_mul_f32_e32 v22, 0x43800000, v27
	v_med3_f32 v14, v14, s19, v1
	v_med3_f32 v22, v22, s19, v1
	v_mov_b32_e32 v89, v163
	v_cvt_pk_fp8_f32 v89, v14, v22
	v_mul_f32_e32 v23, 0x43800000, v63
	v_mul_f32_e32 v14, 0x43800000, v15
	v_med3_f32 v15, v23, s19, v1
	v_med3_f32 v14, v14, s19, v1
	v_cvt_pk_fp8_f32 v89, v15, v14 op_sel:[0,0,1]
	v_mul_f32_e32 v14, 0x43800000, v148
	v_mul_f32_e32 v15, 0x43800000, v152
	v_med3_f32 v14, v14, s19, v1
	v_med3_f32 v15, v15, s19, v1
	v_mov_b32_e32 v90, v163
	v_cvt_pk_fp8_f32 v90, v14, v15
	v_mul_f32_e32 v22, 0x43800000, v160
	v_mul_f32_e32 v14, 0x43800000, v140
	v_med3_f32 v15, v22, s19, v1
	v_med3_f32 v14, v14, s19, v1
	v_cvt_pk_fp8_f32 v90, v15, v14 op_sel:[0,0,1]
	v_mul_f32_e32 v14, 0x43800000, v132
	v_mul_f32_e32 v15, 0x43800000, v136
	v_med3_f32 v14, v14, s19, v1
	v_med3_f32 v15, v15, s19, v1
	v_mov_b32_e32 v91, v163
	v_cvt_pk_fp8_f32 v91, v14, v15
	v_mul_f32_e32 v22, 0x43800000, v156
	v_mul_f32_e32 v14, 0x43800000, v60
	v_med3_f32 v15, v22, s19, v1
	v_med3_f32 v14, v14, s19, v1
	v_cvt_pk_fp8_f32 v91, v15, v14 op_sel:[0,0,1]
	v_mul_f32_e32 v14, 0x43800000, v48
	v_mul_f32_e32 v15, 0x43800000, v56
	v_med3_f32 v14, v14, s19, v1
	v_med3_f32 v15, v15, s19, v1
	v_mov_b32_e32 v92, v163
	v_cvt_pk_fp8_f32 v92, v14, v15
	v_mul_f32_e32 v22, 0x43800000, v144
	v_mul_f32_e32 v14, 0x43800000, v40
	v_med3_f32 v15, v22, s19, v1
	v_med3_f32 v14, v14, s19, v1
	v_cvt_pk_fp8_f32 v92, v15, v14 op_sel:[0,0,1]
	v_mul_f32_e32 v14, 0x43800000, v24
	v_mul_f32_e32 v15, 0x43800000, v28
	v_med3_f32 v14, v14, s19, v1
	v_med3_f32 v15, v15, s19, v1
	v_mov_b32_e32 v93, v163
	v_cvt_pk_fp8_f32 v93, v14, v15
	v_mul_f32_e32 v22, 0x43800000, v64
	v_mul_f32_e32 v14, 0x43800000, v16
	v_med3_f32 v15, v22, s19, v1
	v_med3_f32 v14, v14, s19, v1
	v_cvt_pk_fp8_f32 v93, v15, v14 op_sel:[0,0,1]
	v_mul_f32_e32 v14, 0x43800000, v149
	v_mul_f32_e32 v15, 0x43800000, v153
	v_med3_f32 v14, v14, s19, v1
	v_med3_f32 v15, v15, s19, v1
	v_mov_b32_e32 v22, v163
	v_cvt_pk_fp8_f32 v22, v14, v15
	v_mul_f32_e32 v16, 0x43800000, v161
	v_mul_f32_e32 v14, 0x43800000, v141
	v_med3_f32 v15, v16, s19, v1
	v_med3_f32 v14, v14, s19, v1
	v_cvt_pk_fp8_f32 v22, v15, v14 op_sel:[0,0,1]
	v_mul_f32_e32 v14, 0x43800000, v133
	v_mul_f32_e32 v15, 0x43800000, v137
	v_med3_f32 v14, v14, s19, v1
	v_med3_f32 v15, v15, s19, v1
	v_mov_b32_e32 v23, v163
	v_cvt_pk_fp8_f32 v23, v14, v15
	v_mul_f32_e32 v16, 0x43800000, v157
	v_mul_f32_e32 v14, 0x43800000, v61
	v_med3_f32 v15, v16, s19, v1
	v_med3_f32 v14, v14, s19, v1
	v_cvt_pk_fp8_f32 v23, v15, v14 op_sel:[0,0,1]
	v_mul_f32_e32 v14, 0x43800000, v49
	v_mul_f32_e32 v15, 0x43800000, v57
	v_med3_f32 v14, v14, s19, v1
	v_med3_f32 v15, v15, s19, v1
	v_mov_b32_e32 v24, v163
	v_cvt_pk_fp8_f32 v24, v14, v15
	v_mul_f32_e32 v16, 0x43800000, v145
	v_mul_f32_e32 v14, 0x43800000, v41
	v_med3_f32 v15, v16, s19, v1
	v_med3_f32 v14, v14, s19, v1
	v_cvt_pk_fp8_f32 v24, v15, v14 op_sel:[0,0,1]
	v_mul_f32_e32 v14, 0x43800000, v25
	v_mul_f32_e32 v15, 0x43800000, v29
	v_med3_f32 v14, v14, s19, v1
	v_med3_f32 v15, v15, s19, v1
	v_mov_b32_e32 v25, v163
	v_cvt_pk_fp8_f32 v25, v14, v15
	v_mul_f32_e32 v16, 0x43800000, v65
	v_mul_f32_e32 v14, 0x43800000, v17
	v_med3_f32 v15, v16, s19, v1
	v_med3_f32 v14, v14, s19, v1
	v_cvt_pk_fp8_f32 v25, v15, v14 op_sel:[0,0,1]
	ds_write_b128 v182, v[78:81] offset:34816
	ds_write_b128 v182, v[86:89] offset:35088
	ds_write_b128 v182, v[90:93] offset:35360
	ds_write_b128 v182, v[22:25] offset:35632
	s_waitcnt lgkmcnt(0)
	s_barrier
	s_mov_b32 s2, 0xa00000
	v_add_co_u32_e32 v14, vcc, s2, v180
	s_mov_b32 s2, 0xa02000
	s_nop 0
	v_addc_co_u32_e32 v15, vcc, 0, v181, vcc
	v_add_co_u32_e32 v16, vcc, s2, v180
	s_mov_b32 s2, 0xa04000
	s_nop 0
	v_addc_co_u32_e32 v17, vcc, 0, v181, vcc
	global_load_dwordx4 v[106:109], v[14:15], off sc0 nt
	global_load_dwordx4 v[114:117], v[16:17], off sc0 nt
	v_add_co_u32_e32 v14, vcc, s2, v180
	s_mov_b32 s2, 0xa06000
	s_nop 0
	v_addc_co_u32_e32 v15, vcc, 0, v181, vcc
	v_add_co_u32_e32 v16, vcc, s2, v180
	s_mov_b32 s2, 0xa08000
	s_nop 0
	v_addc_co_u32_e32 v17, vcc, 0, v181, vcc
	global_load_dwordx4 v[126:129], v[14:15], off sc0 nt
	global_load_dwordx4 v[90:93], v[16:17], off sc0 nt
	v_add_co_u32_e32 v14, vcc, s2, v180
	s_mov_b32 s2, 0xa0a000
	s_nop 0
	v_addc_co_u32_e32 v15, vcc, 0, v181, vcc
	v_add_co_u32_e32 v16, vcc, s2, v180
	s_mov_b32 s2, 0xa0c000
	s_nop 0
	v_addc_co_u32_e32 v17, vcc, 0, v181, vcc
	global_load_dwordx4 v[78:81], v[14:15], off sc0 nt
	global_load_dwordx4 v[86:89], v[16:17], off sc0 nt
	v_add_co_u32_e32 v14, vcc, s2, v180
	s_mov_b32 s2, 0xa0e000
	s_nop 0
	v_addc_co_u32_e32 v15, vcc, 0, v181, vcc
	v_add_co_u32_e32 v16, vcc, s2, v180
	s_mov_b32 s2, 0xa10000
	s_nop 0
	v_addc_co_u32_e32 v17, vcc, 0, v181, vcc
	global_load_dwordx4 v[118:121], v[14:15], off sc0 nt
	global_load_dwordx4 v[58:61], v[16:17], off sc0 nt
	v_add_co_u32_e32 v14, vcc, s2, v180
	s_mov_b32 s2, 0xa12000
	s_nop 0
	v_addc_co_u32_e32 v15, vcc, 0, v181, vcc
	v_add_co_u32_e32 v16, vcc, s2, v180
	s_mov_b32 s2, 0xa14000
	s_nop 0
	v_addc_co_u32_e32 v17, vcc, 0, v181, vcc
	global_load_dwordx4 v[46:49], v[14:15], off sc0 nt
	global_load_dwordx4 v[54:57], v[16:17], off sc0 nt
	v_add_co_u32_e32 v14, vcc, s2, v180
	s_mov_b32 s2, 0xa16000
	s_nop 0
	v_addc_co_u32_e32 v15, vcc, 0, v181, vcc
	v_add_co_u32_e32 v16, vcc, s2, v180
	s_mov_b32 s2, 0xa18000
	s_nop 0
	v_addc_co_u32_e32 v17, vcc, 0, v181, vcc
	global_load_dwordx4 v[94:97], v[14:15], off sc0 nt
	global_load_dwordx4 v[38:41], v[16:17], off sc0 nt
	v_add_co_u32_e32 v14, vcc, s2, v180
	s_mov_b32 s2, 0xa1a000
	s_nop 0
	v_addc_co_u32_e32 v15, vcc, 0, v181, vcc
	v_add_co_u32_e32 v16, vcc, s2, v180
	s_mov_b32 s2, 0xa1c000
	s_nop 0
	v_addc_co_u32_e32 v17, vcc, 0, v181, vcc
	global_load_dwordx4 v[22:25], v[14:15], off sc0 nt
	global_load_dwordx4 v[26:29], v[16:17], off sc0 nt
	v_add_co_u32_e32 v14, vcc, s2, v180
	s_mov_b32 s2, 0xa1e000
	s_nop 0
	v_addc_co_u32_e32 v15, vcc, 0, v181, vcc
	v_add_co_u32_e32 v16, vcc, s2, v180
	s_nop 1
	v_addc_co_u32_e32 v17, vcc, 0, v181, vcc
	global_load_dwordx4 v[62:65], v[14:15], off sc0 nt
	s_nop 0
	global_load_dwordx4 v[14:17], v[16:17], off sc0 nt
	ds_read_b128 v[130:133], v168 offset:34816
	ds_read_b128 v[134:137], v170 offset:34816
	ds_read_b128 v[138:141], v174 offset:34816
	ds_read_b128 v[142:145], v176 offset:34816
	s_waitcnt lgkmcnt(3)
	global_store_dwordx4 v[164:165], v[130:133], off offset:768 nt
	s_waitcnt lgkmcnt(2)
	global_store_dwordx4 v[166:167], v[134:137], off offset:768 nt
	s_waitcnt lgkmcnt(1)
	global_store_dwordx4 v[172:173], v[138:141], off offset:768 nt
	s_waitcnt lgkmcnt(0)
	global_store_dwordx4 v[178:179], v[142:145], off offset:768 nt
	s_waitcnt vmcnt(39)
	v_mul_f32_e32 v98, 0x43800000, v98
	s_waitcnt vmcnt(38)
	v_mul_f32_e32 v110, 0x43800000, v110
	v_med3_f32 v98, v98, s19, v1
	v_med3_f32 v110, v110, s19, v1
	v_mov_b32_e32 v130, v163
	v_cvt_pk_fp8_f32 v130, v98, v110
	s_waitcnt vmcnt(35)
	v_mul_f32_e32 v66, 0x43800000, v66
	s_waitcnt vmcnt(34)
	v_mul_f32_e32 v74, 0x43800000, v74
	v_med3_f32 v66, v66, s19, v1
	v_med3_f32 v74, v74, s19, v1
	v_mov_b32_e32 v131, v163
	v_mul_f32_e32 v122, 0x43800000, v122
	v_mul_f32_e32 v82, 0x43800000, v82
	v_cvt_pk_fp8_f32 v131, v66, v74
	s_waitcnt vmcnt(31)
	v_mul_f32_e32 v30, 0x43800000, v30
	s_waitcnt vmcnt(30)
	v_mul_f32_e32 v42, 0x43800000, v42
	v_med3_f32 v98, v122, s19, v1
	v_med3_f32 v82, v82, s19, v1
	v_med3_f32 v30, v30, s19, v1
	v_med3_f32 v42, v42, s19, v1
	v_mov_b32_e32 v132, v163
	v_cvt_pk_fp8_f32 v130, v98, v82 op_sel:[0,0,1]
	v_mul_f32_e32 v82, 0x43800000, v102
	v_mul_f32_e32 v50, 0x43800000, v50
	v_cvt_pk_fp8_f32 v132, v30, v42
	s_waitcnt vmcnt(27)
	v_mul_f32_e32 v6, 0x43800000, v6
	s_waitcnt vmcnt(26)
	v_mul_f32_e32 v10, 0x43800000, v10
	v_med3_f32 v66, v82, s19, v1
	v_med3_f32 v50, v50, s19, v1
	v_med3_f32 v6, v6, s19, v1
	v_med3_f32 v10, v10, s19, v1
	v_mov_b32_e32 v133, v163
	v_cvt_pk_fp8_f32 v131, v66, v50 op_sel:[0,0,1]
	v_mul_f32_e32 v50, 0x43800000, v70
	v_mul_f32_e32 v18, 0x43800000, v18
	v_cvt_pk_fp8_f32 v133, v6, v10
	v_med3_f32 v30, v50, s19, v1
	v_med3_f32 v18, v18, s19, v1
	v_cvt_pk_fp8_f32 v132, v30, v18 op_sel:[0,0,1]
	s_waitcnt vmcnt(25)
	v_mul_f32_e32 v18, 0x43800000, v34
	s_waitcnt vmcnt(24)
	v_mul_f32_e32 v2, 0x43800000, v2
	v_med3_f32 v6, v18, s19, v1
	v_med3_f32 v2, v2, s19, v1
	v_cvt_pk_fp8_f32 v133, v6, v2 op_sel:[0,0,1]
	v_mul_f32_e32 v2, 0x43800000, v99
	v_mul_f32_e32 v6, 0x43800000, v111
	v_med3_f32 v2, v2, s19, v1
	v_med3_f32 v6, v6, s19, v1
	v_mov_b32_e32 v134, v163
	v_cvt_pk_fp8_f32 v134, v2, v6
	v_mul_f32_e32 v10, 0x43800000, v123
	v_mul_f32_e32 v2, 0x43800000, v83
	v_med3_f32 v6, v10, s19, v1
	v_med3_f32 v2, v2, s19, v1
	v_cvt_pk_fp8_f32 v134, v6, v2 op_sel:[0,0,1]
	v_mul_f32_e32 v2, 0x43800000, v67
	v_mul_f32_e32 v6, 0x43800000, v75
	v_med3_f32 v2, v2, s19, v1
	v_med3_f32 v6, v6, s19, v1
	v_mov_b32_e32 v135, v163
	v_cvt_pk_fp8_f32 v135, v2, v6
	v_mul_f32_e32 v10, 0x43800000, v103
	v_mul_f32_e32 v2, 0x43800000, v51
	v_med3_f32 v6, v10, s19, v1
	v_med3_f32 v2, v2, s19, v1
	v_cvt_pk_fp8_f32 v135, v6, v2 op_sel:[0,0,1]
	v_mul_f32_e32 v2, 0x43800000, v31
	v_mul_f32_e32 v6, 0x43800000, v43
	v_med3_f32 v2, v2, s19, v1
	v_med3_f32 v6, v6, s19, v1
	v_mov_b32_e32 v136, v163
	v_cvt_pk_fp8_f32 v136, v2, v6
	v_mul_f32_e32 v10, 0x43800000, v71
	v_mul_f32_e32 v2, 0x43800000, v19
	v_med3_f32 v6, v10, s19, v1
	v_med3_f32 v2, v2, s19, v1
	v_cvt_pk_fp8_f32 v136, v6, v2 op_sel:[0,0,1]
	v_mul_f32_e32 v2, 0x43800000, v7
	v_mul_f32_e32 v6, 0x43800000, v11
	v_med3_f32 v2, v2, s19, v1
	v_med3_f32 v6, v6, s19, v1
	v_mov_b32_e32 v137, v163
	v_cvt_pk_fp8_f32 v137, v2, v6
	v_mul_f32_e32 v7, 0x43800000, v35
	v_mul_f32_e32 v2, 0x43800000, v3
	v_med3_f32 v3, v7, s19, v1
	v_med3_f32 v2, v2, s19, v1
	v_cvt_pk_fp8_f32 v137, v3, v2 op_sel:[0,0,1]
	v_mul_f32_e32 v2, 0x43800000, v100
	v_mul_f32_e32 v3, 0x43800000, v112
	v_med3_f32 v2, v2, s19, v1
	v_med3_f32 v3, v3, s19, v1
	v_mov_b32_e32 v138, v163
	v_cvt_pk_fp8_f32 v138, v2, v3
	v_mul_f32_e32 v6, 0x43800000, v124
	v_mul_f32_e32 v2, 0x43800000, v84
	v_med3_f32 v3, v6, s19, v1
	v_med3_f32 v2, v2, s19, v1
	v_cvt_pk_fp8_f32 v138, v3, v2 op_sel:[0,0,1]
	v_mul_f32_e32 v2, 0x43800000, v68
	v_mul_f32_e32 v3, 0x43800000, v76
	v_med3_f32 v2, v2, s19, v1
	v_med3_f32 v3, v3, s19, v1
	v_mov_b32_e32 v139, v163
	v_cvt_pk_fp8_f32 v139, v2, v3
	v_mul_f32_e32 v6, 0x43800000, v104
	v_mul_f32_e32 v2, 0x43800000, v52
	v_med3_f32 v3, v6, s19, v1
	v_med3_f32 v2, v2, s19, v1
	v_cvt_pk_fp8_f32 v139, v3, v2 op_sel:[0,0,1]
	v_mul_f32_e32 v2, 0x43800000, v32
	v_mul_f32_e32 v3, 0x43800000, v44
	v_med3_f32 v2, v2, s19, v1
	v_med3_f32 v3, v3, s19, v1
	v_mov_b32_e32 v140, v163
	v_cvt_pk_fp8_f32 v140, v2, v3
	v_mul_f32_e32 v6, 0x43800000, v72
	v_mul_f32_e32 v2, 0x43800000, v20
	v_med3_f32 v3, v6, s19, v1
	v_med3_f32 v2, v2, s19, v1
	v_cvt_pk_fp8_f32 v140, v3, v2 op_sel:[0,0,1]
	v_mul_f32_e32 v2, 0x43800000, v8
	v_mul_f32_e32 v3, 0x43800000, v12
	v_med3_f32 v2, v2, s19, v1
	v_med3_f32 v3, v3, s19, v1
	v_mov_b32_e32 v141, v163
	v_cvt_pk_fp8_f32 v141, v2, v3
	v_mul_f32_e32 v6, 0x43800000, v36
	v_mul_f32_e32 v2, 0x43800000, v4
	v_med3_f32 v3, v6, s19, v1
	v_med3_f32 v2, v2, s19, v1
	v_cvt_pk_fp8_f32 v141, v3, v2 op_sel:[0,0,1]
	v_mul_f32_e32 v2, 0x43800000, v101
	v_mul_f32_e32 v3, 0x43800000, v113
	v_med3_f32 v2, v2, s19, v1
	v_med3_f32 v3, v3, s19, v1
	v_mov_b32_e32 v6, v163
	v_cvt_pk_fp8_f32 v6, v2, v3
	v_mul_f32_e32 v4, 0x43800000, v125
	v_mul_f32_e32 v2, 0x43800000, v85
	v_med3_f32 v3, v4, s19, v1
	v_med3_f32 v2, v2, s19, v1
	v_cvt_pk_fp8_f32 v6, v3, v2 op_sel:[0,0,1]
	v_mul_f32_e32 v2, 0x43800000, v69
	v_mul_f32_e32 v3, 0x43800000, v77
	v_med3_f32 v2, v2, s19, v1
	v_med3_f32 v3, v3, s19, v1
	v_mov_b32_e32 v7, v163
	v_cvt_pk_fp8_f32 v7, v2, v3
	v_mul_f32_e32 v4, 0x43800000, v105
	v_mul_f32_e32 v2, 0x43800000, v53
	v_med3_f32 v3, v4, s19, v1
	v_med3_f32 v2, v2, s19, v1
	v_cvt_pk_fp8_f32 v7, v3, v2 op_sel:[0,0,1]
	v_mul_f32_e32 v2, 0x43800000, v33
	v_mul_f32_e32 v3, 0x43800000, v45
	v_med3_f32 v2, v2, s19, v1
	v_med3_f32 v3, v3, s19, v1
	v_mov_b32_e32 v8, v163
	v_cvt_pk_fp8_f32 v8, v2, v3
	v_mul_f32_e32 v4, 0x43800000, v73
	v_mul_f32_e32 v2, 0x43800000, v21
	v_med3_f32 v3, v4, s19, v1
	v_med3_f32 v2, v2, s19, v1
	v_cvt_pk_fp8_f32 v8, v3, v2 op_sel:[0,0,1]
	v_mul_f32_e32 v2, 0x43800000, v9
	v_mul_f32_e32 v3, 0x43800000, v13
	v_med3_f32 v2, v2, s19, v1
	v_med3_f32 v3, v3, s19, v1
	v_mov_b32_e32 v9, v163
	v_cvt_pk_fp8_f32 v9, v2, v3
	v_mul_f32_e32 v4, 0x43800000, v37
	v_mul_f32_e32 v2, 0x43800000, v5
	v_med3_f32 v3, v4, s19, v1
	v_med3_f32 v2, v2, s19, v1
	v_cvt_pk_fp8_f32 v9, v3, v2 op_sel:[0,0,1]
	ds_write_b128 v182, v[130:133]
	ds_write_b128 v182, v[134:137] offset:272
	ds_write_b128 v182, v[138:141] offset:544
	ds_write_b128 v182, v[6:9] offset:816
	s_waitcnt lgkmcnt(0)
	s_barrier
	v_add_co_u32_e32 v2, vcc, s56, v180
	s_mov_b32 s2, 0xc02000
	s_nop 0
	v_addc_co_u32_e32 v3, vcc, 0, v181, vcc
	v_add_co_u32_e32 v4, vcc, s2, v180
	s_mov_b32 s2, 0xc06000
	s_nop 0
	v_addc_co_u32_e32 v5, vcc, 0, v181, vcc
	global_load_dwordx4 v[98:101], v[2:3], off sc0 nt
	global_load_dwordx4 v[110:113], v[4:5], off sc0 nt
	v_add_co_u32_e32 v2, vcc, s57, v180
	s_nop 1
	v_addc_co_u32_e32 v3, vcc, 0, v181, vcc
	v_add_co_u32_e32 v4, vcc, s2, v180
	s_mov_b32 s2, 0xc0a000
	s_nop 0
	v_addc_co_u32_e32 v5, vcc, 0, v181, vcc
	global_load_dwordx4 v[122:125], v[2:3], off sc0 nt
	global_load_dwordx4 v[82:85], v[4:5], off sc0 nt
	v_add_co_u32_e32 v2, vcc, s58, v180
	s_nop 1
	v_addc_co_u32_e32 v3, vcc, 0, v181, vcc
	v_add_co_u32_e32 v4, vcc, s2, v180
	s_mov_b32 s2, 0xc0e000
	s_nop 0
	v_addc_co_u32_e32 v5, vcc, 0, v181, vcc
	global_load_dwordx4 v[66:69], v[2:3], off sc0 nt
	global_load_dwordx4 v[74:77], v[4:5], off sc0 nt
	v_add_co_u32_e32 v2, vcc, s59, v180
	s_nop 1
	v_addc_co_u32_e32 v3, vcc, 0, v181, vcc
	v_add_co_u32_e32 v4, vcc, s2, v180
	s_mov_b32 s2, 0xc12000
	s_nop 0
	v_addc_co_u32_e32 v5, vcc, 0, v181, vcc
	global_load_dwordx4 v[102:105], v[2:3], off sc0 nt
	global_load_dwordx4 v[50:53], v[4:5], off sc0 nt
	v_add_co_u32_e32 v2, vcc, s60, v180
	s_nop 1
	v_addc_co_u32_e32 v3, vcc, 0, v181, vcc
	v_add_co_u32_e32 v4, vcc, s2, v180
	s_mov_b32 s2, 0xc16000
	s_nop 0
	v_addc_co_u32_e32 v5, vcc, 0, v181, vcc
	global_load_dwordx4 v[30:33], v[2:3], off sc0 nt
	global_load_dwordx4 v[42:45], v[4:5], off sc0 nt
	v_add_co_u32_e32 v2, vcc, s61, v180
	s_nop 1
	v_addc_co_u32_e32 v3, vcc, 0, v181, vcc
	v_add_co_u32_e32 v4, vcc, s2, v180
	s_mov_b32 s2, 0xc1a000
	s_nop 0
	v_addc_co_u32_e32 v5, vcc, 0, v181, vcc
	global_load_dwordx4 v[70:73], v[2:3], off sc0 nt
	global_load_dwordx4 v[18:21], v[4:5], off sc0 nt
	v_add_co_u32_e32 v2, vcc, s62, v180
	s_nop 1
	v_addc_co_u32_e32 v3, vcc, 0, v181, vcc
	v_add_co_u32_e32 v4, vcc, s2, v180
	s_mov_b32 s2, 0xc1e000
	s_nop 0
	v_addc_co_u32_e32 v5, vcc, 0, v181, vcc
	global_load_dwordx4 v[6:9], v[2:3], off sc0 nt
	global_load_dwordx4 v[10:13], v[4:5], off sc0 nt
	v_add_co_u32_e32 v2, vcc, s63, v180
	s_nop 1
	v_addc_co_u32_e32 v3, vcc, 0, v181, vcc
	v_add_co_u32_e32 v4, vcc, s2, v180
	s_nop 1
	v_addc_co_u32_e32 v5, vcc, 0, v181, vcc
	global_load_dwordx4 v[34:37], v[2:3], off sc0 nt
	s_nop 0
	global_load_dwordx4 v[2:5], v[4:5], off sc0 nt
	ds_read_b128 v[130:133], v168
	ds_read_b128 v[134:137], v170
	ds_read_b128 v[138:141], v174
	ds_read_b128 v[142:145], v176
	s_waitcnt lgkmcnt(3)
	global_store_dwordx4 v[164:165], v[130:133], off offset:1024 nt
	s_waitcnt lgkmcnt(2)
	global_store_dwordx4 v[166:167], v[134:137], off offset:1024 nt
	s_waitcnt lgkmcnt(1)
	global_store_dwordx4 v[172:173], v[138:141], off offset:1024 nt
	s_waitcnt lgkmcnt(0)
	global_store_dwordx4 v[178:179], v[142:145], off offset:1024 nt
	s_waitcnt vmcnt(39)
	v_mul_f32_e32 v106, 0x43800000, v106
	s_waitcnt vmcnt(38)
	v_mul_f32_e32 v114, 0x43800000, v114
	v_med3_f32 v106, v106, s19, v1
	v_med3_f32 v114, v114, s19, v1
	v_mov_b32_e32 v130, v163
	v_cvt_pk_fp8_f32 v130, v106, v114
	s_waitcnt vmcnt(35)
	v_mul_f32_e32 v78, 0x43800000, v78
	s_waitcnt vmcnt(34)
	v_mul_f32_e32 v86, 0x43800000, v86
	v_med3_f32 v78, v78, s19, v1
	v_med3_f32 v86, v86, s19, v1
	v_mov_b32_e32 v131, v163
	v_mul_f32_e32 v126, 0x43800000, v126
	v_mul_f32_e32 v90, 0x43800000, v90
	v_cvt_pk_fp8_f32 v131, v78, v86
	s_waitcnt vmcnt(31)
	v_mul_f32_e32 v46, 0x43800000, v46
	s_waitcnt vmcnt(30)
	v_mul_f32_e32 v54, 0x43800000, v54
	v_med3_f32 v106, v126, s19, v1
	v_med3_f32 v90, v90, s19, v1
	v_med3_f32 v46, v46, s19, v1
	v_med3_f32 v54, v54, s19, v1
	v_mov_b32_e32 v132, v163
	v_cvt_pk_fp8_f32 v130, v106, v90 op_sel:[0,0,1]
	v_mul_f32_e32 v90, 0x43800000, v118
	v_mul_f32_e32 v58, 0x43800000, v58
	v_cvt_pk_fp8_f32 v132, v46, v54
	s_waitcnt vmcnt(27)
	v_mul_f32_e32 v22, 0x43800000, v22
	s_waitcnt vmcnt(26)
	v_mul_f32_e32 v26, 0x43800000, v26
	v_med3_f32 v78, v90, s19, v1
	v_med3_f32 v58, v58, s19, v1
	v_med3_f32 v22, v22, s19, v1
	v_med3_f32 v26, v26, s19, v1
	v_mov_b32_e32 v133, v163
	v_cvt_pk_fp8_f32 v131, v78, v58 op_sel:[0,0,1]
	v_mul_f32_e32 v58, 0x43800000, v94
	v_mul_f32_e32 v38, 0x43800000, v38
	v_cvt_pk_fp8_f32 v133, v22, v26
	v_med3_f32 v46, v58, s19, v1
	v_med3_f32 v38, v38, s19, v1
	v_cvt_pk_fp8_f32 v132, v46, v38 op_sel:[0,0,1]
	s_waitcnt vmcnt(25)
	v_mul_f32_e32 v38, 0x43800000, v62
	s_waitcnt vmcnt(24)
	v_mul_f32_e32 v14, 0x43800000, v14
	v_med3_f32 v22, v38, s19, v1
	v_med3_f32 v14, v14, s19, v1
	v_cvt_pk_fp8_f32 v133, v22, v14 op_sel:[0,0,1]
	v_mul_f32_e32 v14, 0x43800000, v107
	v_mul_f32_e32 v22, 0x43800000, v115
	v_med3_f32 v14, v14, s19, v1
	v_med3_f32 v22, v22, s19, v1
	v_mov_b32_e32 v134, v163
	v_cvt_pk_fp8_f32 v134, v14, v22
	v_mul_f32_e32 v26, 0x43800000, v127
	v_mul_f32_e32 v14, 0x43800000, v91
	v_med3_f32 v22, v26, s19, v1
	v_med3_f32 v14, v14, s19, v1
	v_cvt_pk_fp8_f32 v134, v22, v14 op_sel:[0,0,1]
	v_mul_f32_e32 v14, 0x43800000, v79
	v_mul_f32_e32 v22, 0x43800000, v87
	v_med3_f32 v14, v14, s19, v1
	v_med3_f32 v22, v22, s19, v1
	v_mov_b32_e32 v135, v163
	v_cvt_pk_fp8_f32 v135, v14, v22
	v_mul_f32_e32 v26, 0x43800000, v119
	v_mul_f32_e32 v14, 0x43800000, v59
	v_med3_f32 v22, v26, s19, v1
	v_med3_f32 v14, v14, s19, v1
	v_cvt_pk_fp8_f32 v135, v22, v14 op_sel:[0,0,1]
	v_mul_f32_e32 v14, 0x43800000, v47
	v_mul_f32_e32 v22, 0x43800000, v55
	v_med3_f32 v14, v14, s19, v1
	v_med3_f32 v22, v22, s19, v1
	v_mov_b32_e32 v136, v163
	v_cvt_pk_fp8_f32 v136, v14, v22
	v_mul_f32_e32 v26, 0x43800000, v95
	v_mul_f32_e32 v14, 0x43800000, v39
	v_med3_f32 v22, v26, s19, v1
	v_med3_f32 v14, v14, s19, v1
	v_cvt_pk_fp8_f32 v136, v22, v14 op_sel:[0,0,1]
	v_mul_f32_e32 v14, 0x43800000, v23
	v_mul_f32_e32 v22, 0x43800000, v27
	v_med3_f32 v14, v14, s19, v1
	v_med3_f32 v22, v22, s19, v1
	v_mov_b32_e32 v137, v163
	v_cvt_pk_fp8_f32 v137, v14, v22
	v_mul_f32_e32 v23, 0x43800000, v63
	v_mul_f32_e32 v14, 0x43800000, v15
	v_med3_f32 v15, v23, s19, v1
	v_med3_f32 v14, v14, s19, v1
	v_cvt_pk_fp8_f32 v137, v15, v14 op_sel:[0,0,1]
	v_mul_f32_e32 v14, 0x43800000, v108
	v_mul_f32_e32 v15, 0x43800000, v116
	v_med3_f32 v14, v14, s19, v1
	v_med3_f32 v15, v15, s19, v1
	v_mov_b32_e32 v138, v163
	v_cvt_pk_fp8_f32 v138, v14, v15
	v_mul_f32_e32 v22, 0x43800000, v128
	v_mul_f32_e32 v14, 0x43800000, v92
	v_med3_f32 v15, v22, s19, v1
	v_med3_f32 v14, v14, s19, v1
	v_cvt_pk_fp8_f32 v138, v15, v14 op_sel:[0,0,1]
	v_mul_f32_e32 v14, 0x43800000, v80
	v_mul_f32_e32 v15, 0x43800000, v88
	v_med3_f32 v14, v14, s19, v1
	v_med3_f32 v15, v15, s19, v1
	v_mov_b32_e32 v139, v163
	v_cvt_pk_fp8_f32 v139, v14, v15
	v_mul_f32_e32 v22, 0x43800000, v120
	v_mul_f32_e32 v14, 0x43800000, v60
	v_med3_f32 v15, v22, s19, v1
	v_med3_f32 v14, v14, s19, v1
	v_cvt_pk_fp8_f32 v139, v15, v14 op_sel:[0,0,1]
	v_mul_f32_e32 v14, 0x43800000, v48
	v_mul_f32_e32 v15, 0x43800000, v56
	v_med3_f32 v14, v14, s19, v1
	v_med3_f32 v15, v15, s19, v1
	v_mov_b32_e32 v140, v163
	v_cvt_pk_fp8_f32 v140, v14, v15
	v_mul_f32_e32 v22, 0x43800000, v96
	v_mul_f32_e32 v14, 0x43800000, v40
	v_med3_f32 v15, v22, s19, v1
	v_med3_f32 v14, v14, s19, v1
	v_cvt_pk_fp8_f32 v140, v15, v14 op_sel:[0,0,1]
	v_mul_f32_e32 v14, 0x43800000, v24
	v_mul_f32_e32 v15, 0x43800000, v28
	v_med3_f32 v14, v14, s19, v1
	v_med3_f32 v15, v15, s19, v1
	v_mov_b32_e32 v141, v163
	v_cvt_pk_fp8_f32 v141, v14, v15
	v_mul_f32_e32 v22, 0x43800000, v64
	v_mul_f32_e32 v14, 0x43800000, v16
	v_med3_f32 v15, v22, s19, v1
	v_med3_f32 v14, v14, s19, v1
	v_cvt_pk_fp8_f32 v141, v15, v14 op_sel:[0,0,1]
	v_mul_f32_e32 v14, 0x43800000, v109
	v_mul_f32_e32 v15, 0x43800000, v117
	v_med3_f32 v14, v14, s19, v1
	v_med3_f32 v15, v15, s19, v1
	v_mov_b32_e32 v22, v163
	v_cvt_pk_fp8_f32 v22, v14, v15
	v_mul_f32_e32 v16, 0x43800000, v129
	v_mul_f32_e32 v14, 0x43800000, v93
	v_med3_f32 v15, v16, s19, v1
	v_med3_f32 v14, v14, s19, v1
	v_cvt_pk_fp8_f32 v22, v15, v14 op_sel:[0,0,1]
	v_mul_f32_e32 v14, 0x43800000, v81
	v_mul_f32_e32 v15, 0x43800000, v89
	v_med3_f32 v14, v14, s19, v1
	v_med3_f32 v15, v15, s19, v1
	v_mov_b32_e32 v23, v163
	v_cvt_pk_fp8_f32 v23, v14, v15
	v_mul_f32_e32 v16, 0x43800000, v121
	v_mul_f32_e32 v14, 0x43800000, v61
	v_med3_f32 v15, v16, s19, v1
	v_med3_f32 v14, v14, s19, v1
	v_cvt_pk_fp8_f32 v23, v15, v14 op_sel:[0,0,1]
	v_mul_f32_e32 v14, 0x43800000, v49
	v_mul_f32_e32 v15, 0x43800000, v57
	v_med3_f32 v14, v14, s19, v1
	v_med3_f32 v15, v15, s19, v1
	v_mov_b32_e32 v24, v163
	v_cvt_pk_fp8_f32 v24, v14, v15
	v_mul_f32_e32 v16, 0x43800000, v97
	v_mul_f32_e32 v14, 0x43800000, v41
	v_med3_f32 v15, v16, s19, v1
	v_med3_f32 v14, v14, s19, v1
	v_cvt_pk_fp8_f32 v24, v15, v14 op_sel:[0,0,1]
	v_mul_f32_e32 v14, 0x43800000, v25
	v_mul_f32_e32 v15, 0x43800000, v29
	v_med3_f32 v14, v14, s19, v1
	v_med3_f32 v15, v15, s19, v1
	v_mov_b32_e32 v25, v163
	v_cvt_pk_fp8_f32 v25, v14, v15
	v_mul_f32_e32 v16, 0x43800000, v65
	v_mul_f32_e32 v14, 0x43800000, v17
	v_med3_f32 v15, v16, s19, v1
	v_med3_f32 v14, v14, s19, v1
	v_cvt_pk_fp8_f32 v25, v15, v14 op_sel:[0,0,1]
	ds_write_b128 v182, v[130:133] offset:34816
	ds_write_b128 v182, v[134:137] offset:35088
	ds_write_b128 v182, v[138:141] offset:35360
	ds_write_b128 v182, v[22:25] offset:35632
	s_waitcnt lgkmcnt(0)
	s_barrier
	s_mov_b32 s2, 0xe00000
	v_add_co_u32_e32 v14, vcc, s2, v180
	s_mov_b32 s2, 0xe02000
	s_nop 0
	v_addc_co_u32_e32 v15, vcc, 0, v181, vcc
	v_add_co_u32_e32 v16, vcc, s2, v180
	s_mov_b32 s2, 0xe04000
	s_nop 0
	v_addc_co_u32_e32 v17, vcc, 0, v181, vcc
	global_load_dwordx4 v[106:109], v[14:15], off sc0 nt
	global_load_dwordx4 v[114:117], v[16:17], off sc0 nt
	v_add_co_u32_e32 v14, vcc, s2, v180
	s_mov_b32 s2, 0xe06000
	s_nop 0
	v_addc_co_u32_e32 v15, vcc, 0, v181, vcc
	v_add_co_u32_e32 v16, vcc, s2, v180
	s_mov_b32 s2, 0xe08000
	s_nop 0
	v_addc_co_u32_e32 v17, vcc, 0, v181, vcc
	global_load_dwordx4 v[126:129], v[14:15], off sc0 nt
	global_load_dwordx4 v[90:93], v[16:17], off sc0 nt
	v_add_co_u32_e32 v14, vcc, s2, v180
	s_mov_b32 s2, 0xe0a000
	s_nop 0
	v_addc_co_u32_e32 v15, vcc, 0, v181, vcc
	v_add_co_u32_e32 v16, vcc, s2, v180
	s_mov_b32 s2, 0xe0c000
	s_nop 0
	v_addc_co_u32_e32 v17, vcc, 0, v181, vcc
	global_load_dwordx4 v[78:81], v[14:15], off sc0 nt
	global_load_dwordx4 v[86:89], v[16:17], off sc0 nt
	v_add_co_u32_e32 v14, vcc, s2, v180
	s_mov_b32 s2, 0xe0e000
	s_nop 0
	v_addc_co_u32_e32 v15, vcc, 0, v181, vcc
	v_add_co_u32_e32 v16, vcc, s2, v180
	s_mov_b32 s2, 0xe10000
	s_nop 0
	v_addc_co_u32_e32 v17, vcc, 0, v181, vcc
	global_load_dwordx4 v[118:121], v[14:15], off sc0 nt
	global_load_dwordx4 v[58:61], v[16:17], off sc0 nt
	v_add_co_u32_e32 v14, vcc, s2, v180
	s_mov_b32 s2, 0xe12000
	s_nop 0
	v_addc_co_u32_e32 v15, vcc, 0, v181, vcc
	v_add_co_u32_e32 v16, vcc, s2, v180
	s_mov_b32 s2, 0xe14000
	s_nop 0
	v_addc_co_u32_e32 v17, vcc, 0, v181, vcc
	global_load_dwordx4 v[46:49], v[14:15], off sc0 nt
	global_load_dwordx4 v[54:57], v[16:17], off sc0 nt
	v_add_co_u32_e32 v14, vcc, s2, v180
	s_mov_b32 s2, 0xe16000
	s_nop 0
	v_addc_co_u32_e32 v15, vcc, 0, v181, vcc
	v_add_co_u32_e32 v16, vcc, s2, v180
	s_mov_b32 s2, 0xe18000
	s_nop 0
	v_addc_co_u32_e32 v17, vcc, 0, v181, vcc
	global_load_dwordx4 v[94:97], v[14:15], off sc0 nt
	global_load_dwordx4 v[38:41], v[16:17], off sc0 nt
	v_add_co_u32_e32 v14, vcc, s2, v180
	s_mov_b32 s2, 0xe1a000
	s_nop 0
	v_addc_co_u32_e32 v15, vcc, 0, v181, vcc
	v_add_co_u32_e32 v16, vcc, s2, v180
	s_mov_b32 s2, 0xe1c000
	s_nop 0
	v_addc_co_u32_e32 v17, vcc, 0, v181, vcc
	global_load_dwordx4 v[22:25], v[14:15], off sc0 nt
	global_load_dwordx4 v[26:29], v[16:17], off sc0 nt
	v_add_co_u32_e32 v14, vcc, s2, v180
	s_mov_b32 s2, 0xe1e000
	s_nop 0
	v_addc_co_u32_e32 v15, vcc, 0, v181, vcc
	v_add_co_u32_e32 v16, vcc, s2, v180
	s_nop 1
	v_addc_co_u32_e32 v17, vcc, 0, v181, vcc
	global_load_dwordx4 v[62:65], v[14:15], off sc0 nt
	s_nop 0
	global_load_dwordx4 v[14:17], v[16:17], off sc0 nt
	ds_read_b128 v[130:133], v168 offset:34816
	ds_read_b128 v[134:137], v170 offset:34816
	ds_read_b128 v[138:141], v174 offset:34816
	ds_read_b128 v[142:145], v176 offset:34816
	s_waitcnt lgkmcnt(3)
	global_store_dwordx4 v[164:165], v[130:133], off offset:1280 nt
	s_waitcnt lgkmcnt(2)
	global_store_dwordx4 v[166:167], v[134:137], off offset:1280 nt
	s_waitcnt lgkmcnt(1)
	global_store_dwordx4 v[172:173], v[138:141], off offset:1280 nt
	s_waitcnt lgkmcnt(0)
	global_store_dwordx4 v[178:179], v[142:145], off offset:1280 nt
	s_waitcnt vmcnt(39)
	v_mul_f32_e32 v98, 0x43800000, v98
	s_waitcnt vmcnt(38)
	v_mul_f32_e32 v110, 0x43800000, v110
	v_med3_f32 v98, v98, s19, v1
	v_med3_f32 v110, v110, s19, v1
	v_mov_b32_e32 v130, v163
	v_cvt_pk_fp8_f32 v130, v98, v110
	s_waitcnt vmcnt(35)
	v_mul_f32_e32 v66, 0x43800000, v66
	s_waitcnt vmcnt(34)
	v_mul_f32_e32 v74, 0x43800000, v74
	v_med3_f32 v66, v66, s19, v1
	v_med3_f32 v74, v74, s19, v1
	v_mov_b32_e32 v131, v163
	v_mul_f32_e32 v122, 0x43800000, v122
	v_mul_f32_e32 v82, 0x43800000, v82
	v_cvt_pk_fp8_f32 v131, v66, v74
	s_waitcnt vmcnt(31)
	v_mul_f32_e32 v30, 0x43800000, v30
	s_waitcnt vmcnt(30)
	v_mul_f32_e32 v42, 0x43800000, v42
	v_med3_f32 v98, v122, s19, v1
	v_med3_f32 v82, v82, s19, v1
	v_med3_f32 v30, v30, s19, v1
	v_med3_f32 v42, v42, s19, v1
	v_mov_b32_e32 v132, v163
	v_cvt_pk_fp8_f32 v130, v98, v82 op_sel:[0,0,1]
	v_mul_f32_e32 v82, 0x43800000, v102
	v_mul_f32_e32 v50, 0x43800000, v50
	v_cvt_pk_fp8_f32 v132, v30, v42
	s_waitcnt vmcnt(27)
	v_mul_f32_e32 v6, 0x43800000, v6
	s_waitcnt vmcnt(26)
	v_mul_f32_e32 v10, 0x43800000, v10
	v_med3_f32 v66, v82, s19, v1
	v_med3_f32 v50, v50, s19, v1
	v_med3_f32 v6, v6, s19, v1
	v_med3_f32 v10, v10, s19, v1
	v_mov_b32_e32 v133, v163
	v_cvt_pk_fp8_f32 v131, v66, v50 op_sel:[0,0,1]
	v_mul_f32_e32 v50, 0x43800000, v70
	v_mul_f32_e32 v18, 0x43800000, v18
	v_cvt_pk_fp8_f32 v133, v6, v10
	v_med3_f32 v30, v50, s19, v1
	v_med3_f32 v18, v18, s19, v1
	v_cvt_pk_fp8_f32 v132, v30, v18 op_sel:[0,0,1]
	s_waitcnt vmcnt(25)
	v_mul_f32_e32 v18, 0x43800000, v34
	s_waitcnt vmcnt(24)
	v_mul_f32_e32 v2, 0x43800000, v2
	v_med3_f32 v6, v18, s19, v1
	v_med3_f32 v2, v2, s19, v1
	v_cvt_pk_fp8_f32 v133, v6, v2 op_sel:[0,0,1]
	v_mul_f32_e32 v2, 0x43800000, v99
	v_mul_f32_e32 v6, 0x43800000, v111
	v_med3_f32 v2, v2, s19, v1
	v_med3_f32 v6, v6, s19, v1
	v_mov_b32_e32 v134, v163
	v_cvt_pk_fp8_f32 v134, v2, v6
	v_mul_f32_e32 v10, 0x43800000, v123
	v_mul_f32_e32 v2, 0x43800000, v83
	v_med3_f32 v6, v10, s19, v1
	v_med3_f32 v2, v2, s19, v1
	v_cvt_pk_fp8_f32 v134, v6, v2 op_sel:[0,0,1]
	v_mul_f32_e32 v2, 0x43800000, v67
	v_mul_f32_e32 v6, 0x43800000, v75
	v_med3_f32 v2, v2, s19, v1
	v_med3_f32 v6, v6, s19, v1
	v_mov_b32_e32 v135, v163
	v_cvt_pk_fp8_f32 v135, v2, v6
	v_mul_f32_e32 v10, 0x43800000, v103
	v_mul_f32_e32 v2, 0x43800000, v51
	v_med3_f32 v6, v10, s19, v1
	v_med3_f32 v2, v2, s19, v1
	v_cvt_pk_fp8_f32 v135, v6, v2 op_sel:[0,0,1]
	v_mul_f32_e32 v2, 0x43800000, v31
	v_mul_f32_e32 v6, 0x43800000, v43
	v_med3_f32 v2, v2, s19, v1
	v_med3_f32 v6, v6, s19, v1
	v_mov_b32_e32 v136, v163
	v_cvt_pk_fp8_f32 v136, v2, v6
	v_mul_f32_e32 v10, 0x43800000, v71
	v_mul_f32_e32 v2, 0x43800000, v19
	v_med3_f32 v6, v10, s19, v1
	v_med3_f32 v2, v2, s19, v1
	v_cvt_pk_fp8_f32 v136, v6, v2 op_sel:[0,0,1]
	v_mul_f32_e32 v2, 0x43800000, v7
	v_mul_f32_e32 v6, 0x43800000, v11
	v_med3_f32 v2, v2, s19, v1
	v_med3_f32 v6, v6, s19, v1
	v_mov_b32_e32 v137, v163
	v_cvt_pk_fp8_f32 v137, v2, v6
	v_mul_f32_e32 v7, 0x43800000, v35
	v_mul_f32_e32 v2, 0x43800000, v3
	v_med3_f32 v3, v7, s19, v1
	v_med3_f32 v2, v2, s19, v1
	v_cvt_pk_fp8_f32 v137, v3, v2 op_sel:[0,0,1]
	v_mul_f32_e32 v2, 0x43800000, v100
	v_mul_f32_e32 v3, 0x43800000, v112
	v_med3_f32 v2, v2, s19, v1
	v_med3_f32 v3, v3, s19, v1
	v_mov_b32_e32 v138, v163
	v_cvt_pk_fp8_f32 v138, v2, v3
	v_mul_f32_e32 v6, 0x43800000, v124
	v_mul_f32_e32 v2, 0x43800000, v84
	v_med3_f32 v3, v6, s19, v1
	v_med3_f32 v2, v2, s19, v1
	v_cvt_pk_fp8_f32 v138, v3, v2 op_sel:[0,0,1]
	v_mul_f32_e32 v2, 0x43800000, v68
	v_mul_f32_e32 v3, 0x43800000, v76
	v_med3_f32 v2, v2, s19, v1
	v_med3_f32 v3, v3, s19, v1
	v_mov_b32_e32 v139, v163
	v_cvt_pk_fp8_f32 v139, v2, v3
	v_mul_f32_e32 v6, 0x43800000, v104
	v_mul_f32_e32 v2, 0x43800000, v52
	v_med3_f32 v3, v6, s19, v1
	v_med3_f32 v2, v2, s19, v1
	v_cvt_pk_fp8_f32 v139, v3, v2 op_sel:[0,0,1]
	v_mul_f32_e32 v2, 0x43800000, v32
	v_mul_f32_e32 v3, 0x43800000, v44
	v_med3_f32 v2, v2, s19, v1
	v_med3_f32 v3, v3, s19, v1
	v_mov_b32_e32 v140, v163
	v_cvt_pk_fp8_f32 v140, v2, v3
	v_mul_f32_e32 v6, 0x43800000, v72
	v_mul_f32_e32 v2, 0x43800000, v20
	v_med3_f32 v3, v6, s19, v1
	v_med3_f32 v2, v2, s19, v1
	v_cvt_pk_fp8_f32 v140, v3, v2 op_sel:[0,0,1]
	v_mul_f32_e32 v2, 0x43800000, v8
	v_mul_f32_e32 v3, 0x43800000, v12
	v_med3_f32 v2, v2, s19, v1
	v_med3_f32 v3, v3, s19, v1
	v_mov_b32_e32 v141, v163
	v_cvt_pk_fp8_f32 v141, v2, v3
	v_mul_f32_e32 v6, 0x43800000, v36
	v_mul_f32_e32 v2, 0x43800000, v4
	v_med3_f32 v3, v6, s19, v1
	v_med3_f32 v2, v2, s19, v1
	v_cvt_pk_fp8_f32 v141, v3, v2 op_sel:[0,0,1]
	v_mul_f32_e32 v2, 0x43800000, v101
	v_mul_f32_e32 v3, 0x43800000, v113
	v_med3_f32 v2, v2, s19, v1
	v_med3_f32 v3, v3, s19, v1
	v_mov_b32_e32 v6, v163
	v_cvt_pk_fp8_f32 v6, v2, v3
	v_mul_f32_e32 v4, 0x43800000, v125
	v_mul_f32_e32 v2, 0x43800000, v85
	v_med3_f32 v3, v4, s19, v1
	v_med3_f32 v2, v2, s19, v1
	v_cvt_pk_fp8_f32 v6, v3, v2 op_sel:[0,0,1]
	v_mul_f32_e32 v2, 0x43800000, v69
	v_mul_f32_e32 v3, 0x43800000, v77
	v_med3_f32 v2, v2, s19, v1
	v_med3_f32 v3, v3, s19, v1
	v_mov_b32_e32 v7, v163
	v_cvt_pk_fp8_f32 v7, v2, v3
	v_mul_f32_e32 v4, 0x43800000, v105
	v_mul_f32_e32 v2, 0x43800000, v53
	v_med3_f32 v3, v4, s19, v1
	v_med3_f32 v2, v2, s19, v1
	v_cvt_pk_fp8_f32 v7, v3, v2 op_sel:[0,0,1]
	v_mul_f32_e32 v2, 0x43800000, v33
	v_mul_f32_e32 v3, 0x43800000, v45
	v_med3_f32 v2, v2, s19, v1
	v_med3_f32 v3, v3, s19, v1
	v_mov_b32_e32 v8, v163
	v_cvt_pk_fp8_f32 v8, v2, v3
	v_mul_f32_e32 v4, 0x43800000, v73
	v_mul_f32_e32 v2, 0x43800000, v21
	v_med3_f32 v3, v4, s19, v1
	v_med3_f32 v2, v2, s19, v1
	v_cvt_pk_fp8_f32 v8, v3, v2 op_sel:[0,0,1]
	v_mul_f32_e32 v2, 0x43800000, v9
	v_mul_f32_e32 v3, 0x43800000, v13
	v_med3_f32 v2, v2, s19, v1
	v_med3_f32 v3, v3, s19, v1
	v_mov_b32_e32 v9, v163
	v_cvt_pk_fp8_f32 v9, v2, v3
	v_mul_f32_e32 v4, 0x43800000, v37
	v_mul_f32_e32 v2, 0x43800000, v5
	v_med3_f32 v3, v4, s19, v1
	v_med3_f32 v2, v2, s19, v1
	v_cvt_pk_fp8_f32 v9, v3, v2 op_sel:[0,0,1]
	ds_write_b128 v182, v[130:133]
	ds_write_b128 v182, v[134:137] offset:272
	ds_write_b128 v182, v[138:141] offset:544
	ds_write_b128 v182, v[6:9] offset:816
	s_waitcnt lgkmcnt(0)
	s_barrier
	ds_read_b128 v[2:5], v168
	ds_read_b128 v[6:9], v170
	ds_read_b128 v[10:13], v174
	ds_read_b128 v[18:21], v176
	s_waitcnt lgkmcnt(3)
	global_store_dwordx4 v[164:165], v[2:5], off offset:1536 nt
	s_waitcnt lgkmcnt(2)
	global_store_dwordx4 v[166:167], v[6:9], off offset:1536 nt
	s_waitcnt lgkmcnt(1)
	global_store_dwordx4 v[172:173], v[10:13], off offset:1536 nt
	s_waitcnt lgkmcnt(0)
	global_store_dwordx4 v[178:179], v[18:21], off offset:1536 nt
	s_waitcnt vmcnt(23)
	v_mul_f32_e32 v2, 0x43800000, v106
	s_waitcnt vmcnt(22)
	v_mul_f32_e32 v3, 0x43800000, v114
	v_med3_f32 v5, v2, s19, v1
	v_med3_f32 v3, v3, s19, v1
	v_mov_b32_e32 v2, v163
	v_cvt_pk_fp8_f32 v2, v5, v3
	s_waitcnt vmcnt(21)
	v_mul_f32_e32 v4, 0x43800000, v126
	s_waitcnt vmcnt(20)
	v_mul_f32_e32 v3, 0x43800000, v90
	v_med3_f32 v4, v4, s19, v1
	v_med3_f32 v3, v3, s19, v1
	v_cvt_pk_fp8_f32 v2, v4, v3 op_sel:[0,0,1]
	s_waitcnt vmcnt(19)
	v_mul_f32_e32 v3, 0x43800000, v78
	s_waitcnt vmcnt(18)
	v_mul_f32_e32 v4, 0x43800000, v86
	v_med3_f32 v6, v3, s19, v1
	v_med3_f32 v4, v4, s19, v1
	v_mov_b32_e32 v3, v163
	v_cvt_pk_fp8_f32 v3, v6, v4
	s_waitcnt vmcnt(17)
	v_mul_f32_e32 v5, 0x43800000, v118
	s_waitcnt vmcnt(16)
	v_mul_f32_e32 v4, 0x43800000, v58
	v_med3_f32 v5, v5, s19, v1
	v_med3_f32 v4, v4, s19, v1
	v_cvt_pk_fp8_f32 v3, v5, v4 op_sel:[0,0,1]
	s_waitcnt vmcnt(15)
	v_mul_f32_e32 v4, 0x43800000, v46
	s_waitcnt vmcnt(14)
	v_mul_f32_e32 v5, 0x43800000, v54
	v_med3_f32 v7, v4, s19, v1
	v_med3_f32 v5, v5, s19, v1
	v_mov_b32_e32 v4, v163
	v_cvt_pk_fp8_f32 v4, v7, v5
	s_waitcnt vmcnt(13)
	v_mul_f32_e32 v6, 0x43800000, v94
	s_waitcnt vmcnt(12)
	v_mul_f32_e32 v5, 0x43800000, v38
	v_med3_f32 v6, v6, s19, v1
	v_med3_f32 v5, v5, s19, v1
	v_cvt_pk_fp8_f32 v4, v6, v5 op_sel:[0,0,1]
	s_waitcnt vmcnt(11)
	v_mul_f32_e32 v5, 0x43800000, v22
	s_waitcnt vmcnt(10)
	v_mul_f32_e32 v6, 0x43800000, v26
	v_med3_f32 v8, v5, s19, v1
	v_med3_f32 v6, v6, s19, v1
	v_mov_b32_e32 v5, v163
	v_cvt_pk_fp8_f32 v5, v8, v6
	s_waitcnt vmcnt(9)
	v_mul_f32_e32 v7, 0x43800000, v62
	s_waitcnt vmcnt(8)
	v_mul_f32_e32 v6, 0x43800000, v14
	v_med3_f32 v7, v7, s19, v1
	v_med3_f32 v6, v6, s19, v1
	v_cvt_pk_fp8_f32 v5, v7, v6 op_sel:[0,0,1]
	v_mul_f32_e32 v6, 0x43800000, v107
	v_mul_f32_e32 v7, 0x43800000, v115
	v_med3_f32 v9, v6, s19, v1
	v_med3_f32 v7, v7, s19, v1
	v_mov_b32_e32 v6, v163
	v_cvt_pk_fp8_f32 v6, v9, v7
	v_mul_f32_e32 v8, 0x43800000, v127
	v_mul_f32_e32 v7, 0x43800000, v91
	v_med3_f32 v8, v8, s19, v1
	v_med3_f32 v7, v7, s19, v1
	v_cvt_pk_fp8_f32 v6, v8, v7 op_sel:[0,0,1]
	v_mul_f32_e32 v7, 0x43800000, v79
	v_mul_f32_e32 v8, 0x43800000, v87
	v_med3_f32 v10, v7, s19, v1
	v_med3_f32 v8, v8, s19, v1
	v_mov_b32_e32 v7, v163
	v_cvt_pk_fp8_f32 v7, v10, v8
	v_mul_f32_e32 v9, 0x43800000, v119
	v_mul_f32_e32 v8, 0x43800000, v59
	v_med3_f32 v9, v9, s19, v1
	v_med3_f32 v8, v8, s19, v1
	v_cvt_pk_fp8_f32 v7, v9, v8 op_sel:[0,0,1]
	v_mul_f32_e32 v8, 0x43800000, v47
	v_mul_f32_e32 v9, 0x43800000, v55
	v_med3_f32 v11, v8, s19, v1
	v_med3_f32 v9, v9, s19, v1
	v_mov_b32_e32 v8, v163
	v_cvt_pk_fp8_f32 v8, v11, v9
	v_mul_f32_e32 v10, 0x43800000, v95
	v_mul_f32_e32 v9, 0x43800000, v39
	v_med3_f32 v10, v10, s19, v1
	v_med3_f32 v9, v9, s19, v1
	v_cvt_pk_fp8_f32 v8, v10, v9 op_sel:[0,0,1]
	v_mul_f32_e32 v9, 0x43800000, v23
	v_mul_f32_e32 v10, 0x43800000, v27
	v_med3_f32 v12, v9, s19, v1
	v_med3_f32 v10, v10, s19, v1
	v_mov_b32_e32 v9, v163
	v_cvt_pk_fp8_f32 v9, v12, v10
	v_mul_f32_e32 v11, 0x43800000, v63
	v_mul_f32_e32 v10, 0x43800000, v15
	v_med3_f32 v11, v11, s19, v1
	v_med3_f32 v10, v10, s19, v1
	v_cvt_pk_fp8_f32 v9, v11, v10 op_sel:[0,0,1]
	v_mul_f32_e32 v10, 0x43800000, v108
	v_mul_f32_e32 v11, 0x43800000, v116
	v_med3_f32 v13, v10, s19, v1
	v_med3_f32 v11, v11, s19, v1
	v_mov_b32_e32 v10, v163
	v_cvt_pk_fp8_f32 v10, v13, v11
	v_mul_f32_e32 v12, 0x43800000, v128
	v_mul_f32_e32 v11, 0x43800000, v92
	v_med3_f32 v12, v12, s19, v1
	v_med3_f32 v11, v11, s19, v1
	v_cvt_pk_fp8_f32 v10, v12, v11 op_sel:[0,0,1]
	v_mul_f32_e32 v11, 0x43800000, v80
	v_mul_f32_e32 v12, 0x43800000, v88
	v_med3_f32 v14, v11, s19, v1
	v_med3_f32 v12, v12, s19, v1
	v_mov_b32_e32 v11, v163
	v_cvt_pk_fp8_f32 v11, v14, v12
	v_mul_f32_e32 v13, 0x43800000, v120
	v_mul_f32_e32 v12, 0x43800000, v60
	v_med3_f32 v13, v13, s19, v1
	v_med3_f32 v12, v12, s19, v1
	v_cvt_pk_fp8_f32 v11, v13, v12 op_sel:[0,0,1]
	v_mul_f32_e32 v12, 0x43800000, v48
	v_mul_f32_e32 v13, 0x43800000, v56
	v_med3_f32 v15, v12, s19, v1
	v_med3_f32 v13, v13, s19, v1
	v_mov_b32_e32 v12, v163
	v_cvt_pk_fp8_f32 v12, v15, v13
	v_mul_f32_e32 v14, 0x43800000, v96
	v_mul_f32_e32 v13, 0x43800000, v40
	v_med3_f32 v14, v14, s19, v1
	v_med3_f32 v13, v13, s19, v1
	v_cvt_pk_fp8_f32 v12, v14, v13 op_sel:[0,0,1]
	v_mul_f32_e32 v13, 0x43800000, v24
	v_mul_f32_e32 v14, 0x43800000, v28
	v_med3_f32 v18, v13, s19, v1
	v_med3_f32 v14, v14, s19, v1
	v_mov_b32_e32 v13, v163
	v_cvt_pk_fp8_f32 v13, v18, v14
	v_mul_f32_e32 v15, 0x43800000, v64
	v_mul_f32_e32 v14, 0x43800000, v16
	v_med3_f32 v15, v15, s19, v1
	v_med3_f32 v14, v14, s19, v1
	v_cvt_pk_fp8_f32 v13, v15, v14 op_sel:[0,0,1]
	v_mul_f32_e32 v14, 0x43800000, v109
	v_mul_f32_e32 v15, 0x43800000, v117
	v_med3_f32 v14, v14, s19, v1
	v_med3_f32 v15, v15, s19, v1
	v_mov_b32_e32 v18, v163
	v_cvt_pk_fp8_f32 v18, v14, v15
	v_mul_f32_e32 v16, 0x43800000, v129
	v_mul_f32_e32 v14, 0x43800000, v93
	v_med3_f32 v15, v16, s19, v1
	v_med3_f32 v14, v14, s19, v1
	v_cvt_pk_fp8_f32 v18, v15, v14 op_sel:[0,0,1]
	v_mul_f32_e32 v14, 0x43800000, v81
	v_mul_f32_e32 v15, 0x43800000, v89
	v_med3_f32 v14, v14, s19, v1
	v_med3_f32 v15, v15, s19, v1
	v_mov_b32_e32 v19, v163
	v_cvt_pk_fp8_f32 v19, v14, v15
	v_mul_f32_e32 v16, 0x43800000, v121
	v_mul_f32_e32 v14, 0x43800000, v61
	v_med3_f32 v15, v16, s19, v1
	v_med3_f32 v14, v14, s19, v1
	v_cvt_pk_fp8_f32 v19, v15, v14 op_sel:[0,0,1]
	v_mul_f32_e32 v14, 0x43800000, v49
	v_mul_f32_e32 v15, 0x43800000, v57
	v_med3_f32 v14, v14, s19, v1
	v_med3_f32 v15, v15, s19, v1
	v_mov_b32_e32 v20, v163
	v_cvt_pk_fp8_f32 v20, v14, v15
	v_mul_f32_e32 v16, 0x43800000, v97
	v_mul_f32_e32 v14, 0x43800000, v41
	v_med3_f32 v15, v16, s19, v1
	v_med3_f32 v14, v14, s19, v1
	v_cvt_pk_fp8_f32 v20, v15, v14 op_sel:[0,0,1]
	v_mul_f32_e32 v14, 0x43800000, v25
	v_mul_f32_e32 v15, 0x43800000, v29
	v_med3_f32 v14, v14, s19, v1
	v_med3_f32 v15, v15, s19, v1
	v_mov_b32_e32 v21, v163
	v_cvt_pk_fp8_f32 v21, v14, v15
	v_mul_f32_e32 v16, 0x43800000, v65
	v_mul_f32_e32 v14, 0x43800000, v17
	v_med3_f32 v15, v16, s19, v1
	v_med3_f32 v14, v14, s19, v1
	v_cvt_pk_fp8_f32 v21, v15, v14 op_sel:[0,0,1]
	ds_write_b128 v182, v[2:5] offset:34816
	ds_write_b128 v182, v[6:9] offset:35088
	ds_write_b128 v182, v[10:13] offset:35360
	ds_write_b128 v182, v[18:21] offset:35632
	s_waitcnt lgkmcnt(0)
	s_barrier
	ds_read_b128 v[2:5], v168 offset:34816
	ds_read_b128 v[6:9], v170 offset:34816
	ds_read_b128 v[10:13], v174 offset:34816
	ds_read_b128 v[14:17], v176 offset:34816
	s_waitcnt lgkmcnt(3)
	global_store_dwordx4 v[164:165], v[2:5], off offset:1792 nt
	s_waitcnt lgkmcnt(2)
	global_store_dwordx4 v[166:167], v[6:9], off offset:1792 nt
	s_waitcnt lgkmcnt(1)
	global_store_dwordx4 v[172:173], v[10:13], off offset:1792 nt
	s_waitcnt lgkmcnt(0)
	global_store_dwordx4 v[178:179], v[14:17], off offset:1792 nt
	s_barrier
	s_mov_b64 s[10:11], 0
.LBB0_165:
	s_andn2_b64 vcc, exec, s[10:11]
	s_cbranch_vccnz .LBB0_162
	s_ashr_i32 s10, s76, 5
	s_ashr_i32 s11, s10, 31
	v_readlane_b32 s84, v254, 4
	s_and_b32 s2, s76, 31
	s_lshl_b64 s[68:69], s[10:11], 25
	v_readlane_b32 s86, v254, 6
	v_readlane_b32 s87, v254, 7
	s_add_u32 s34, s86, s68
	s_addc_u32 s35, s87, s69
	s_lshl_b32 s68, s76, 6
	s_lshl_b32 s69, s76, 11
	s_and_b32 s68, s68, 0x780
	s_and_b32 s69, s69, 0x800
	s_or_b32 s68, s68, s69
	s_lshl_b32 s68, s68, 2
	s_add_u32 s68, s34, s68
	s_addc_u32 s69, s35, 0
	s_lshl_b32 s2, s2, 18
	s_lshl_b64 s[10:11], s[10:11], 23
	s_add_u32 s10, s4, s10
	v_mov_b32_e32 v130, v0
	s_addc_u32 s11, s5, s11
	s_add_u32 s10, s10, s2
	v_readfirstlane_b32 s8, v130
	s_addc_u32 s11, s11, 0
	s_ashr_i32 s2, s8, 1
	s_waitcnt lgkmcnt(1)
	v_lshrrev_b32_e32 v2, 1, v130
	s_andn2_b32 s2, s2, 31
	v_and_b32_e32 v131, 16, v2
	v_or_b32_e32 v2, s2, v131
	v_ashrrev_i32_e32 v3, 31, v2
	s_waitcnt lgkmcnt(0)
	v_lshlrev_b32_e32 v4, 2, v130
	v_lshlrev_b64 v[2:3], 14, v[2:3]
	v_and_b32_e32 v136, 0x7c, v4
	v_lshl_add_u64 v[2:3], s[68:69], 0, v[2:3]
	v_lshlrev_b32_e32 v162, 2, v136
	v_lshl_add_u64 v[180:181], v[2:3], 0, v[162:163]
	v_add_co_u32_e32 v2, vcc, s12, v180
	s_mov_b32 s8, 0x20000
	s_nop 0
	v_addc_co_u32_e32 v3, vcc, 0, v181, vcc
	global_load_dwordx4 v[114:117], v[180:181], off sc0 nt
	global_load_dwordx4 v[118:121], v[2:3], off sc0 nt
	v_add_co_u32_e32 v2, vcc, s13, v180
	v_readlane_b32 s85, v254, 5
	s_nop 0
	v_addc_co_u32_e32 v3, vcc, 0, v181, vcc
	v_add_co_u32_e32 v4, vcc, s14, v180
	v_readlane_b32 s88, v254, 8
	s_nop 0
	v_addc_co_u32_e32 v5, vcc, 0, v181, vcc
	global_load_dwordx4 v[122:125], v[2:3], off sc0 nt
	global_load_dwordx4 v[126:129], v[4:5], off sc0 nt
	v_add_co_u32_e32 v2, vcc, s15, v180
	v_readlane_b32 s89, v254, 9
	s_nop 0
	v_addc_co_u32_e32 v3, vcc, 0, v181, vcc
	v_add_co_u32_e32 v4, vcc, s16, v180
	v_readlane_b32 s90, v254, 10
	s_nop 0
	v_addc_co_u32_e32 v5, vcc, 0, v181, vcc
	global_load_dwordx4 v[94:97], v[2:3], off sc0 nt
	global_load_dwordx4 v[102:105], v[4:5], off sc0 nt
	v_add_co_u32_e32 v2, vcc, s17, v180
	v_readlane_b32 s91, v254, 11
	s_nop 0
	v_addc_co_u32_e32 v3, vcc, 0, v181, vcc
	v_add_co_u32_e32 v4, vcc, s18, v180
	s_nop 1
	v_addc_co_u32_e32 v5, vcc, 0, v181, vcc
	global_load_dwordx4 v[106:109], v[2:3], off sc0 nt
	global_load_dwordx4 v[110:113], v[4:5], off sc0 nt
	v_add_co_u32_e32 v2, vcc, s8, v180
	s_mov_b32 s8, 0x24000
	s_nop 0
	v_addc_co_u32_e32 v3, vcc, 0, v181, vcc
	v_add_co_u32_e32 v4, vcc, s8, v180
	s_mov_b32 s8, 0x28000
	s_nop 0
	v_addc_co_u32_e32 v5, vcc, 0, v181, vcc
	global_load_dwordx4 v[74:77], v[2:3], off sc0 nt
	global_load_dwordx4 v[82:85], v[4:5], off sc0 nt
	v_add_co_u32_e32 v2, vcc, s8, v180
	s_mov_b32 s8, 0x2c000
	s_nop 0
	v_addc_co_u32_e32 v3, vcc, 0, v181, vcc
	v_add_co_u32_e32 v4, vcc, s8, v180
	s_mov_b32 s8, 0x30000
	s_nop 0
	v_addc_co_u32_e32 v5, vcc, 0, v181, vcc
	global_load_dwordx4 v[90:93], v[2:3], off sc0 nt
	global_load_dwordx4 v[98:101], v[4:5], off sc0 nt
	v_add_co_u32_e32 v2, vcc, s8, v180
	s_mov_b32 s8, 0x34000
	s_nop 0
	v_addc_co_u32_e32 v3, vcc, 0, v181, vcc
	v_add_co_u32_e32 v4, vcc, s8, v180
	s_mov_b32 s8, 0x38000
	s_nop 0
	v_addc_co_u32_e32 v5, vcc, 0, v181, vcc
	global_load_dwordx4 v[66:69], v[2:3], off sc0 nt
	global_load_dwordx4 v[70:73], v[4:5], off sc0 nt
	v_add_co_u32_e32 v2, vcc, s8, v180
	s_mov_b32 s8, 0x3c000
	s_nop 0
	v_addc_co_u32_e32 v3, vcc, 0, v181, vcc
	v_add_co_u32_e32 v4, vcc, s8, v180
	s_mov_b32 s8, 0x420000
	s_nop 0
	v_addc_co_u32_e32 v5, vcc, 0, v181, vcc
	global_load_dwordx4 v[78:81], v[2:3], off sc0 nt
	global_load_dwordx4 v[86:89], v[4:5], off sc0 nt
	v_add_co_u32_e32 v2, vcc, s21, v180
	s_nop 1
	v_addc_co_u32_e32 v3, vcc, 0, v181, vcc
	v_add_co_u32_e32 v4, vcc, s22, v180
	s_nop 1
	v_addc_co_u32_e32 v5, vcc, 0, v181, vcc
	global_load_dwordx4 v[54:57], v[2:3], off sc0 nt
	global_load_dwordx4 v[58:61], v[4:5], off sc0 nt
	v_add_co_u32_e32 v2, vcc, s23, v180
	s_nop 1
	v_addc_co_u32_e32 v3, vcc, 0, v181, vcc
	v_add_co_u32_e32 v4, vcc, s24, v180
	s_nop 1
	v_addc_co_u32_e32 v5, vcc, 0, v181, vcc
	global_load_dwordx4 v[62:65], v[2:3], off sc0 nt
	global_load_dwordx4 v[46:49], v[4:5], off sc0 nt
	v_add_co_u32_e32 v2, vcc, s25, v180
	s_nop 1
	v_addc_co_u32_e32 v3, vcc, 0, v181, vcc
	v_add_co_u32_e32 v4, vcc, s26, v180
	s_nop 1
	v_addc_co_u32_e32 v5, vcc, 0, v181, vcc
	global_load_dwordx4 v[34:37], v[2:3], off sc0 nt
	global_load_dwordx4 v[38:41], v[4:5], off sc0 nt
	v_add_co_u32_e32 v2, vcc, s27, v180
	s_nop 1
	v_addc_co_u32_e32 v3, vcc, 0, v181, vcc
	v_add_co_u32_e32 v4, vcc, s28, v180
	s_nop 1
	v_addc_co_u32_e32 v5, vcc, 0, v181, vcc
	global_load_dwordx4 v[50:53], v[2:3], off sc0 nt
	global_load_dwordx4 v[26:29], v[4:5], off sc0 nt
	v_add_co_u32_e32 v2, vcc, s8, v180
	s_mov_b32 s8, 0x424000
	s_nop 0
	v_addc_co_u32_e32 v3, vcc, 0, v181, vcc
	v_add_co_u32_e32 v4, vcc, s8, v180
	s_mov_b32 s8, 0x428000
	s_nop 0
	v_addc_co_u32_e32 v5, vcc, 0, v181, vcc
	global_load_dwordx4 v[18:21], v[2:3], off sc0 nt
	global_load_dwordx4 v[22:25], v[4:5], off sc0 nt
	v_add_co_u32_e32 v2, vcc, s8, v180
	s_mov_b32 s8, 0x42c000
	s_nop 0
	v_addc_co_u32_e32 v3, vcc, 0, v181, vcc
	v_add_co_u32_e32 v4, vcc, s8, v180
	s_mov_b32 s8, 0x430000
	s_nop 0
	v_addc_co_u32_e32 v5, vcc, 0, v181, vcc
	global_load_dwordx4 v[42:45], v[2:3], off sc0 nt
	global_load_dwordx4 v[14:17], v[4:5], off sc0 nt
	v_add_co_u32_e32 v2, vcc, s8, v180
	s_mov_b32 s8, 0x434000
	s_nop 0
	v_addc_co_u32_e32 v3, vcc, 0, v181, vcc
	v_add_co_u32_e32 v4, vcc, s8, v180
	s_mov_b32 s8, 0x438000
	s_nop 0
	v_addc_co_u32_e32 v5, vcc, 0, v181, vcc
	global_load_dwordx4 v[6:9], v[2:3], off sc0 nt
	global_load_dwordx4 v[10:13], v[4:5], off sc0 nt
	v_add_co_u32_e32 v2, vcc, s8, v180
	s_mov_b32 s8, 0x43c000
	s_nop 0
	v_addc_co_u32_e32 v3, vcc, 0, v181, vcc
	v_add_co_u32_e32 v4, vcc, s8, v180
	s_nop 1
	v_addc_co_u32_e32 v5, vcc, 0, v181, vcc
	global_load_dwordx4 v[30:33], v[2:3], off sc0 nt
	s_nop 0
	global_load_dwordx4 v[2:5], v[4:5], off sc0 nt
	s_waitcnt vmcnt(31)
	v_mul_f32_e32 v114, 0x43800000, v114
	s_waitcnt vmcnt(30)
	v_mul_f32_e32 v118, 0x43800000, v118
	s_waitcnt vmcnt(27)
	v_mul_f32_e32 v94, 0x43800000, v94
	s_waitcnt vmcnt(26)
	v_mul_f32_e32 v102, 0x43800000, v102
	s_waitcnt vmcnt(23)
	v_mul_f32_e32 v74, 0x43800000, v74
	s_waitcnt vmcnt(22)
	v_mul_f32_e32 v82, 0x43800000, v82
	s_waitcnt vmcnt(19)
	v_mul_f32_e32 v66, 0x43800000, v66
	s_waitcnt vmcnt(18)
	v_mul_f32_e32 v70, 0x43800000, v70
	v_med3_f32 v114, v114, s19, v1
	v_med3_f32 v118, v118, s19, v1
	v_mov_b32_e32 v132, v163
	v_med3_f32 v94, v94, s19, v1
	v_med3_f32 v102, v102, s19, v1
	v_mov_b32_e32 v133, v163
	v_med3_f32 v74, v74, s19, v1
	v_med3_f32 v82, v82, s19, v1
	v_mov_b32_e32 v134, v163
	v_med3_f32 v66, v66, s19, v1
	v_med3_f32 v70, v70, s19, v1
	v_mov_b32_e32 v135, v163
	v_cvt_pk_fp8_f32 v132, v114, v118
	v_cvt_pk_fp8_f32 v133, v94, v102
	v_cvt_pk_fp8_f32 v134, v74, v82
	v_cvt_pk_fp8_f32 v135, v66, v70
	v_mul_f32_e32 v122, 0x43800000, v122
	v_mul_f32_e32 v126, 0x43800000, v126
	v_mul_f32_e32 v106, 0x43800000, v106
	v_mul_f32_e32 v110, 0x43800000, v110
	v_mul_f32_e32 v90, 0x43800000, v90
	v_mul_f32_e32 v94, 0x43800000, v98
	s_waitcnt vmcnt(17)
	v_mul_f32_e32 v74, 0x43800000, v78
	s_waitcnt vmcnt(16)
	v_mul_f32_e32 v78, 0x43800000, v86
	v_med3_f32 v122, v122, s19, v1
	v_med3_f32 v126, v126, s19, v1
	v_med3_f32 v106, v106, s19, v1
	v_med3_f32 v110, v110, s19, v1
	v_med3_f32 v90, v90, s19, v1
	v_med3_f32 v94, v94, s19, v1
	v_med3_f32 v74, v74, s19, v1
	v_med3_f32 v78, v78, s19, v1
	v_cvt_pk_fp8_f32 v132, v122, v126 op_sel:[0,0,1]
	v_cvt_pk_fp8_f32 v133, v106, v110 op_sel:[0,0,1]
	v_cvt_pk_fp8_f32 v134, v90, v94 op_sel:[0,0,1]
	v_cvt_pk_fp8_f32 v135, v74, v78 op_sel:[0,0,1]
	s_add_i32 s2, s2, 0
	v_mul_u32_u24_e32 v66, 0x110, v136
	v_add3_u32 v182, s2, v131, v66
	v_mul_f32_e32 v66, 0x43800000, v115
	v_mul_f32_e32 v70, 0x43800000, v119
	ds_write_b128 v182, v[132:135]
	v_med3_f32 v66, v66, s19, v1
	v_med3_f32 v70, v70, s19, v1
	v_mov_b32_e32 v132, v163
	v_cvt_pk_fp8_f32 v132, v66, v70
	v_mul_f32_e32 v66, 0x43800000, v95
	v_mul_f32_e32 v70, 0x43800000, v103
	v_med3_f32 v66, v66, s19, v1
	v_med3_f32 v70, v70, s19, v1
	v_mov_b32_e32 v133, v163
	v_cvt_pk_fp8_f32 v133, v66, v70
	v_mul_f32_e32 v66, 0x43800000, v75
	v_mul_f32_e32 v70, 0x43800000, v83
	v_med3_f32 v66, v66, s19, v1
	v_med3_f32 v70, v70, s19, v1
	v_mov_b32_e32 v134, v163
	v_mul_f32_e32 v74, 0x43800000, v123
	v_mul_f32_e32 v78, 0x43800000, v127
	v_cvt_pk_fp8_f32 v134, v66, v70
	v_mul_f32_e32 v66, 0x43800000, v67
	v_mul_f32_e32 v67, 0x43800000, v71
	v_med3_f32 v74, v74, s19, v1
	v_med3_f32 v78, v78, s19, v1
	v_med3_f32 v66, v66, s19, v1
	v_med3_f32 v67, v67, s19, v1
	v_mov_b32_e32 v135, v163
	v_cvt_pk_fp8_f32 v132, v74, v78 op_sel:[0,0,1]
	v_mul_f32_e32 v74, 0x43800000, v107
	v_mul_f32_e32 v78, 0x43800000, v111
	v_cvt_pk_fp8_f32 v135, v66, v67
	v_med3_f32 v74, v74, s19, v1
	v_med3_f32 v78, v78, s19, v1
	v_cvt_pk_fp8_f32 v133, v74, v78 op_sel:[0,0,1]
	v_mul_f32_e32 v74, 0x43800000, v91
	v_mul_f32_e32 v75, 0x43800000, v99
	v_mul_f32_e32 v70, 0x43800000, v79
	v_mul_f32_e32 v71, 0x43800000, v87
	v_med3_f32 v74, v74, s19, v1
	v_med3_f32 v75, v75, s19, v1
	v_med3_f32 v70, v70, s19, v1
	v_med3_f32 v71, v71, s19, v1
	v_cvt_pk_fp8_f32 v134, v74, v75 op_sel:[0,0,1]
	v_cvt_pk_fp8_f32 v135, v70, v71 op_sel:[0,0,1]
	v_mul_f32_e32 v66, 0x43800000, v116
	v_mul_f32_e32 v67, 0x43800000, v120
	v_med3_f32 v66, v66, s19, v1
	ds_write_b128 v182, v[132:135] offset:272
	v_med3_f32 v67, v67, s19, v1
	v_mov_b32_e32 v132, v163
	v_cvt_pk_fp8_f32 v132, v66, v67
	v_mul_f32_e32 v66, 0x43800000, v96
	v_mul_f32_e32 v67, 0x43800000, v104
	v_med3_f32 v66, v66, s19, v1
	v_med3_f32 v67, v67, s19, v1
	v_mov_b32_e32 v133, v163
	v_mul_f32_e32 v70, 0x43800000, v124
	v_mul_f32_e32 v71, 0x43800000, v128
	v_cvt_pk_fp8_f32 v133, v66, v67
	v_mul_f32_e32 v66, 0x43800000, v76
	v_mul_f32_e32 v67, 0x43800000, v84
	v_med3_f32 v70, v70, s19, v1
	v_med3_f32 v71, v71, s19, v1
	v_med3_f32 v66, v66, s19, v1
	v_med3_f32 v67, v67, s19, v1
	v_mov_b32_e32 v134, v163
	v_cvt_pk_fp8_f32 v132, v70, v71 op_sel:[0,0,1]
	v_mul_f32_e32 v70, 0x43800000, v108
	v_mul_f32_e32 v71, 0x43800000, v112
	v_cvt_pk_fp8_f32 v134, v66, v67
	v_med3_f32 v70, v70, s19, v1
	v_med3_f32 v71, v71, s19, v1
	v_mul_f32_e32 v66, 0x43800000, v68
	v_mul_f32_e32 v67, 0x43800000, v72
	v_cvt_pk_fp8_f32 v133, v70, v71 op_sel:[0,0,1]
	v_mul_f32_e32 v70, 0x43800000, v92
	v_mul_f32_e32 v71, 0x43800000, v100
	v_med3_f32 v66, v66, s19, v1
	v_med3_f32 v67, v67, s19, v1
	v_mov_b32_e32 v135, v163
	v_med3_f32 v70, v70, s19, v1
	v_med3_f32 v71, v71, s19, v1
	v_cvt_pk_fp8_f32 v135, v66, v67
	v_mul_f32_e32 v66, 0x43800000, v117
	v_mul_f32_e32 v67, 0x43800000, v121
	v_cvt_pk_fp8_f32 v134, v70, v71 op_sel:[0,0,1]
	v_med3_f32 v71, v66, s19, v1
	v_med3_f32 v67, v67, s19, v1
	v_mov_b32_e32 v66, v163
	v_mul_f32_e32 v68, 0x43800000, v80
	v_mul_f32_e32 v70, 0x43800000, v88
	v_cvt_pk_fp8_f32 v66, v71, v67
	v_med3_f32 v68, v68, s19, v1
	v_med3_f32 v70, v70, s19, v1
	v_cvt_pk_fp8_f32 v135, v68, v70 op_sel:[0,0,1]
	v_mul_f32_e32 v68, 0x43800000, v125
	v_mul_f32_e32 v70, 0x43800000, v129
	v_med3_f32 v68, v68, s19, v1
	v_med3_f32 v70, v70, s19, v1
	v_cvt_pk_fp8_f32 v66, v68, v70 op_sel:[0,0,1]
	v_mul_f32_e32 v67, 0x43800000, v97
	v_mul_f32_e32 v68, 0x43800000, v105
	v_med3_f32 v72, v67, s19, v1
	v_med3_f32 v68, v68, s19, v1
	v_mov_b32_e32 v67, v163
	v_cvt_pk_fp8_f32 v67, v72, v68
	v_mul_f32_e32 v70, 0x43800000, v109
	v_mul_f32_e32 v71, 0x43800000, v113
	v_med3_f32 v70, v70, s19, v1
	v_med3_f32 v71, v71, s19, v1
	v_cvt_pk_fp8_f32 v67, v70, v71 op_sel:[0,0,1]
	v_mul_f32_e32 v68, 0x43800000, v77
	v_mul_f32_e32 v70, 0x43800000, v85
	v_med3_f32 v74, v68, s19, v1
	v_med3_f32 v70, v70, s19, v1
	v_mov_b32_e32 v68, v163
	v_cvt_pk_fp8_f32 v68, v74, v70
	v_mul_f32_e32 v69, 0x43800000, v69
	v_mul_f32_e32 v70, 0x43800000, v73
	v_med3_f32 v73, v69, s19, v1
	v_med3_f32 v70, v70, s19, v1
	v_mov_b32_e32 v69, v163
	v_mul_f32_e32 v71, 0x43800000, v93
	v_mul_f32_e32 v72, 0x43800000, v101
	v_cvt_pk_fp8_f32 v69, v73, v70
	v_med3_f32 v71, v71, s19, v1
	v_med3_f32 v72, v72, s19, v1
	v_cvt_pk_fp8_f32 v68, v71, v72 op_sel:[0,0,1]
	v_mul_f32_e32 v71, 0x43800000, v81
	v_mul_f32_e32 v72, 0x43800000, v89
	v_med3_f32 v71, v71, s19, v1
	v_med3_f32 v72, v72, s19, v1
	v_cvt_pk_fp8_f32 v69, v71, v72 op_sel:[0,0,1]
	ds_write_b128 v182, v[132:135] offset:544
	v_ashrrev_i32_e32 v126, 4, v130
	v_ashrrev_i32_e32 v127, 31, v126
	ds_write_b128 v182, v[66:69] offset:816
	v_lshlrev_b32_e32 v66, 4, v130
	v_and_b32_e32 v162, 0xf0, v66
	v_add_u32_e32 v66, 0x200, v130
	v_ashrrev_i32_e32 v134, 4, v66
	v_add_u32_e32 v66, 0x400, v130
	v_ashrrev_i32_e32 v142, 4, v66
	v_add_u32_e32 v66, 0x600, v130
	v_ashrrev_i32_e32 v130, 4, v66
	v_ashrrev_i32_e32 v135, 31, v134
	v_ashrrev_i32_e32 v143, 31, v142
	v_ashrrev_i32_e32 v131, 31, v130
	s_waitcnt lgkmcnt(0)
	s_barrier
	v_lshlrev_b64 v[132:133], 11, v[126:127]
	v_lshlrev_b64 v[136:137], 11, v[134:135]
	v_lshlrev_b64 v[144:145], 11, v[142:143]
	v_lshlrev_b64 v[146:147], 11, v[130:131]
	v_add_co_u32_e32 v66, vcc, s29, v180
	s_mov_b32 s2, 0x820000
	s_nop 0
	v_addc_co_u32_e32 v67, vcc, 0, v181, vcc
	v_add_co_u32_e32 v68, vcc, s30, v180
	s_nop 1
	v_addc_co_u32_e32 v69, vcc, 0, v181, vcc
	global_load_dwordx4 v[118:121], v[66:67], off sc0 nt
	global_load_dwordx4 v[122:125], v[68:69], off sc0 nt
	v_add_co_u32_e32 v66, vcc, s31, v180
	s_nop 1
	v_addc_co_u32_e32 v67, vcc, 0, v181, vcc
	v_add_co_u32_e32 v68, vcc, s33, v180
	s_nop 1
	v_addc_co_u32_e32 v69, vcc, 0, v181, vcc
	global_load_dwordx4 v[138:141], v[66:67], off sc0 nt
	global_load_dwordx4 v[110:113], v[68:69], off sc0 nt
	v_add_co_u32_e32 v66, vcc, s50, v180
	s_nop 1
	v_addc_co_u32_e32 v67, vcc, 0, v181, vcc
	v_add_co_u32_e32 v68, vcc, s51, v180
	s_nop 1
	v_addc_co_u32_e32 v69, vcc, 0, v181, vcc
	global_load_dwordx4 v[98:101], v[66:67], off sc0 nt
	global_load_dwordx4 v[102:105], v[68:69], off sc0 nt
	v_add_co_u32_e32 v66, vcc, s54, v180
	s_nop 1
	v_addc_co_u32_e32 v67, vcc, 0, v181, vcc
	v_add_co_u32_e32 v68, vcc, s55, v180
	s_nop 1
	v_addc_co_u32_e32 v69, vcc, 0, v181, vcc
	global_load_dwordx4 v[114:117], v[66:67], off sc0 nt
	global_load_dwordx4 v[90:93], v[68:69], off sc0 nt
	v_add_co_u32_e32 v66, vcc, s2, v180
	s_mov_b32 s2, 0x824000
	s_nop 0
	v_addc_co_u32_e32 v67, vcc, 0, v181, vcc
	v_add_co_u32_e32 v68, vcc, s2, v180
	s_mov_b32 s2, 0x828000
	s_nop 0
	v_addc_co_u32_e32 v69, vcc, 0, v181, vcc
	global_load_dwordx4 v[82:85], v[66:67], off sc0 nt
	global_load_dwordx4 v[86:89], v[68:69], off sc0 nt
	v_add_co_u32_e32 v66, vcc, s2, v180
	s_mov_b32 s2, 0x82c000
	s_nop 0
	v_addc_co_u32_e32 v67, vcc, 0, v181, vcc
	v_add_co_u32_e32 v68, vcc, s2, v180
	s_mov_b32 s2, 0x830000
	s_nop 0
	v_addc_co_u32_e32 v69, vcc, 0, v181, vcc
	global_load_dwordx4 v[106:109], v[66:67], off sc0 nt
	global_load_dwordx4 v[78:81], v[68:69], off sc0 nt
	v_add_co_u32_e32 v66, vcc, s2, v180
	s_mov_b32 s2, 0x834000
	s_nop 0
	v_addc_co_u32_e32 v67, vcc, 0, v181, vcc
	v_add_co_u32_e32 v68, vcc, s2, v180
	s_mov_b32 s2, 0x838000
	s_nop 0
	v_addc_co_u32_e32 v69, vcc, 0, v181, vcc
	global_load_dwordx4 v[70:73], v[66:67], off sc0 nt
	global_load_dwordx4 v[74:77], v[68:69], off sc0 nt
	v_add_co_u32_e32 v66, vcc, s2, v180
	s_mov_b32 s2, 0x83c000
	s_nop 0
	v_addc_co_u32_e32 v67, vcc, 0, v181, vcc
	v_add_co_u32_e32 v68, vcc, s2, v180
	s_nop 1
	v_addc_co_u32_e32 v69, vcc, 0, v181, vcc
	global_load_dwordx4 v[94:97], v[66:67], off sc0 nt
	s_nop 0
	global_load_dwordx4 v[66:69], v[68:69], off sc0 nt
	v_add_u32_e32 v148, 0, v162
	v_lshl_add_u64 v[150:151], s[10:11], 0, v[162:163]
	v_mad_u64_u32 v[168:169], s[10:11], v126, s20, v[148:149]
	ds_read_b128 v[126:129], v168
	v_lshl_add_u64 v[164:165], v[150:151], 0, v[132:133]
	v_mad_u64_u32 v[170:171], s[10:11], v134, s20, v[148:149]
	v_lshl_add_u64 v[166:167], v[150:151], 0, v[136:137]
	s_waitcnt lgkmcnt(0)
	global_store_dwordx4 v[164:165], v[126:129], off nt
	ds_read_b128 v[126:129], v170
	v_mad_u64_u32 v[174:175], s[10:11], v142, s20, v[148:149]
	v_lshl_add_u64 v[172:173], v[150:151], 0, v[144:145]
	v_mad_u64_u32 v[176:177], s[10:11], v130, s20, v[148:149]
	s_waitcnt lgkmcnt(0)
	global_store_dwordx4 v[166:167], v[126:129], off nt
	ds_read_b128 v[126:129], v174
	v_lshl_add_u64 v[178:179], v[150:151], 0, v[146:147]
	s_waitcnt lgkmcnt(0)
	global_store_dwordx4 v[172:173], v[126:129], off nt
	ds_read_b128 v[126:129], v176
	s_waitcnt lgkmcnt(0)
	global_store_dwordx4 v[178:179], v[126:129], off nt
	s_waitcnt vmcnt(35)
	v_mul_f32_e32 v54, 0x43800000, v54
	s_waitcnt vmcnt(34)
	v_mul_f32_e32 v58, 0x43800000, v58
	v_med3_f32 v54, v54, s19, v1
	v_med3_f32 v58, v58, s19, v1
	v_mov_b32_e32 v126, v163
	v_cvt_pk_fp8_f32 v126, v54, v58
	s_waitcnt vmcnt(31)
	v_mul_f32_e32 v34, 0x43800000, v34
	s_waitcnt vmcnt(30)
	v_mul_f32_e32 v38, 0x43800000, v38
	v_med3_f32 v34, v34, s19, v1
	v_med3_f32 v38, v38, s19, v1
	v_mov_b32_e32 v127, v163
	v_mul_f32_e32 v62, 0x43800000, v62
	v_mul_f32_e32 v46, 0x43800000, v46
	v_cvt_pk_fp8_f32 v127, v34, v38
	s_waitcnt vmcnt(27)
	v_mul_f32_e32 v18, 0x43800000, v18
	s_waitcnt vmcnt(26)
	v_mul_f32_e32 v22, 0x43800000, v22
	v_med3_f32 v54, v62, s19, v1
	v_med3_f32 v46, v46, s19, v1
	v_med3_f32 v18, v18, s19, v1
	v_med3_f32 v22, v22, s19, v1
	v_mov_b32_e32 v128, v163
	v_cvt_pk_fp8_f32 v126, v54, v46 op_sel:[0,0,1]
	v_mul_f32_e32 v46, 0x43800000, v50
	v_mul_f32_e32 v26, 0x43800000, v26
	v_cvt_pk_fp8_f32 v128, v18, v22
	s_waitcnt vmcnt(23)
	v_mul_f32_e32 v6, 0x43800000, v6
	s_waitcnt vmcnt(22)
	v_mul_f32_e32 v10, 0x43800000, v10
	v_med3_f32 v34, v46, s19, v1
	v_med3_f32 v26, v26, s19, v1
	v_med3_f32 v6, v6, s19, v1
	v_med3_f32 v10, v10, s19, v1
	v_mov_b32_e32 v129, v163
	v_cvt_pk_fp8_f32 v127, v34, v26 op_sel:[0,0,1]
	v_mul_f32_e32 v26, 0x43800000, v42
	v_mul_f32_e32 v14, 0x43800000, v14
	v_cvt_pk_fp8_f32 v129, v6, v10
	v_med3_f32 v18, v26, s19, v1
	v_med3_f32 v14, v14, s19, v1
	v_cvt_pk_fp8_f32 v128, v18, v14 op_sel:[0,0,1]
	s_waitcnt vmcnt(21)
	v_mul_f32_e32 v14, 0x43800000, v30
	s_waitcnt vmcnt(20)
	v_mul_f32_e32 v2, 0x43800000, v2
	v_med3_f32 v6, v14, s19, v1
	v_med3_f32 v2, v2, s19, v1
	v_cvt_pk_fp8_f32 v129, v6, v2 op_sel:[0,0,1]
	v_mul_f32_e32 v2, 0x43800000, v55
	v_mul_f32_e32 v6, 0x43800000, v59
	v_med3_f32 v2, v2, s19, v1
	v_med3_f32 v6, v6, s19, v1
	v_mov_b32_e32 v130, v163
	v_cvt_pk_fp8_f32 v130, v2, v6
	v_mul_f32_e32 v10, 0x43800000, v63
	v_mul_f32_e32 v2, 0x43800000, v47
	v_med3_f32 v6, v10, s19, v1
	v_med3_f32 v2, v2, s19, v1
	v_cvt_pk_fp8_f32 v130, v6, v2 op_sel:[0,0,1]
	v_mul_f32_e32 v2, 0x43800000, v35
	v_mul_f32_e32 v6, 0x43800000, v39
	v_med3_f32 v2, v2, s19, v1
	v_med3_f32 v6, v6, s19, v1
	v_mov_b32_e32 v131, v163
	v_cvt_pk_fp8_f32 v131, v2, v6
	v_mul_f32_e32 v10, 0x43800000, v51
	v_mul_f32_e32 v2, 0x43800000, v27
	v_med3_f32 v6, v10, s19, v1
	v_med3_f32 v2, v2, s19, v1
	v_cvt_pk_fp8_f32 v131, v6, v2 op_sel:[0,0,1]
	v_mul_f32_e32 v2, 0x43800000, v19
	v_mul_f32_e32 v6, 0x43800000, v23
	v_med3_f32 v2, v2, s19, v1
	v_med3_f32 v6, v6, s19, v1
	v_mov_b32_e32 v132, v163
	v_cvt_pk_fp8_f32 v132, v2, v6
	v_mul_f32_e32 v10, 0x43800000, v43
	v_mul_f32_e32 v2, 0x43800000, v15
	v_med3_f32 v6, v10, s19, v1
	v_med3_f32 v2, v2, s19, v1
	v_cvt_pk_fp8_f32 v132, v6, v2 op_sel:[0,0,1]
	v_mul_f32_e32 v2, 0x43800000, v7
	v_mul_f32_e32 v6, 0x43800000, v11
	v_med3_f32 v2, v2, s19, v1
	v_med3_f32 v6, v6, s19, v1
	v_mov_b32_e32 v133, v163
	v_cvt_pk_fp8_f32 v133, v2, v6
	v_mul_f32_e32 v7, 0x43800000, v31
	v_mul_f32_e32 v2, 0x43800000, v3
	v_med3_f32 v3, v7, s19, v1
	v_med3_f32 v2, v2, s19, v1
	v_cvt_pk_fp8_f32 v133, v3, v2 op_sel:[0,0,1]
	v_mul_f32_e32 v2, 0x43800000, v56
	v_mul_f32_e32 v3, 0x43800000, v60
	v_med3_f32 v2, v2, s19, v1
	v_med3_f32 v3, v3, s19, v1
	v_mov_b32_e32 v134, v163
	v_cvt_pk_fp8_f32 v134, v2, v3
	v_mul_f32_e32 v6, 0x43800000, v64
	v_mul_f32_e32 v2, 0x43800000, v48
	v_med3_f32 v3, v6, s19, v1
	v_med3_f32 v2, v2, s19, v1
	v_cvt_pk_fp8_f32 v134, v3, v2 op_sel:[0,0,1]
	v_mul_f32_e32 v2, 0x43800000, v36
	v_mul_f32_e32 v3, 0x43800000, v40
	v_med3_f32 v2, v2, s19, v1
	v_med3_f32 v3, v3, s19, v1
	v_mov_b32_e32 v135, v163
	v_cvt_pk_fp8_f32 v135, v2, v3
	v_mul_f32_e32 v6, 0x43800000, v52
	v_mul_f32_e32 v2, 0x43800000, v28
	v_med3_f32 v3, v6, s19, v1
	v_med3_f32 v2, v2, s19, v1
	v_cvt_pk_fp8_f32 v135, v3, v2 op_sel:[0,0,1]
	v_mul_f32_e32 v2, 0x43800000, v20
	v_mul_f32_e32 v3, 0x43800000, v24
	v_med3_f32 v2, v2, s19, v1
	v_med3_f32 v3, v3, s19, v1
	v_mov_b32_e32 v136, v163
	v_cvt_pk_fp8_f32 v136, v2, v3
	v_mul_f32_e32 v6, 0x43800000, v44
	v_mul_f32_e32 v2, 0x43800000, v16
	v_med3_f32 v3, v6, s19, v1
	v_med3_f32 v2, v2, s19, v1
	v_cvt_pk_fp8_f32 v136, v3, v2 op_sel:[0,0,1]
	v_mul_f32_e32 v2, 0x43800000, v8
	v_mul_f32_e32 v3, 0x43800000, v12
	v_med3_f32 v2, v2, s19, v1
	v_med3_f32 v3, v3, s19, v1
	v_mov_b32_e32 v137, v163
	v_cvt_pk_fp8_f32 v137, v2, v3
	v_mul_f32_e32 v6, 0x43800000, v32
	v_mul_f32_e32 v2, 0x43800000, v4
	v_med3_f32 v3, v6, s19, v1
	v_med3_f32 v2, v2, s19, v1
	v_cvt_pk_fp8_f32 v137, v3, v2 op_sel:[0,0,1]
	v_mul_f32_e32 v2, 0x43800000, v57
	v_mul_f32_e32 v3, 0x43800000, v61
	v_med3_f32 v2, v2, s19, v1
	v_med3_f32 v3, v3, s19, v1
	v_mov_b32_e32 v6, v163
	v_cvt_pk_fp8_f32 v6, v2, v3
	v_mul_f32_e32 v4, 0x43800000, v65
	v_mul_f32_e32 v2, 0x43800000, v49
	v_med3_f32 v3, v4, s19, v1
	v_med3_f32 v2, v2, s19, v1
	v_cvt_pk_fp8_f32 v6, v3, v2 op_sel:[0,0,1]
	v_mul_f32_e32 v2, 0x43800000, v37
	v_mul_f32_e32 v3, 0x43800000, v41
	v_med3_f32 v2, v2, s19, v1
	v_med3_f32 v3, v3, s19, v1
	v_mov_b32_e32 v7, v163
	v_cvt_pk_fp8_f32 v7, v2, v3
	v_mul_f32_e32 v4, 0x43800000, v53
	v_mul_f32_e32 v2, 0x43800000, v29
	v_med3_f32 v3, v4, s19, v1
	v_med3_f32 v2, v2, s19, v1
	v_cvt_pk_fp8_f32 v7, v3, v2 op_sel:[0,0,1]
	v_mul_f32_e32 v2, 0x43800000, v21
	v_mul_f32_e32 v3, 0x43800000, v25
	v_med3_f32 v2, v2, s19, v1
	v_med3_f32 v3, v3, s19, v1
	v_mov_b32_e32 v8, v163
	v_cvt_pk_fp8_f32 v8, v2, v3
	v_mul_f32_e32 v4, 0x43800000, v45
	v_mul_f32_e32 v2, 0x43800000, v17
	v_med3_f32 v3, v4, s19, v1
	v_med3_f32 v2, v2, s19, v1
	v_cvt_pk_fp8_f32 v8, v3, v2 op_sel:[0,0,1]
	v_mul_f32_e32 v2, 0x43800000, v9
	v_mul_f32_e32 v3, 0x43800000, v13
	v_med3_f32 v2, v2, s19, v1
	v_med3_f32 v3, v3, s19, v1
	v_mov_b32_e32 v9, v163
	v_cvt_pk_fp8_f32 v9, v2, v3
	v_mul_f32_e32 v4, 0x43800000, v33
	v_mul_f32_e32 v2, 0x43800000, v5
	v_med3_f32 v3, v4, s19, v1
	v_med3_f32 v2, v2, s19, v1
	v_cvt_pk_fp8_f32 v9, v3, v2 op_sel:[0,0,1]
	ds_write_b128 v182, v[126:129] offset:34816
	ds_write_b128 v182, v[130:133] offset:35088
	ds_write_b128 v182, v[134:137] offset:35360
	ds_write_b128 v182, v[6:9] offset:35632
	s_waitcnt lgkmcnt(0)
	s_barrier
	v_add_co_u32_e32 v2, vcc, s56, v180
	s_mov_b32 s2, 0xc20000
	s_nop 0
	v_addc_co_u32_e32 v3, vcc, 0, v181, vcc
	v_add_co_u32_e32 v4, vcc, s57, v180
	s_nop 1
	v_addc_co_u32_e32 v5, vcc, 0, v181, vcc
	global_load_dwordx4 v[150:153], v[2:3], off sc0 nt
	global_load_dwordx4 v[154:157], v[4:5], off sc0 nt
	v_add_co_u32_e32 v2, vcc, s58, v180
	s_nop 1
	v_addc_co_u32_e32 v3, vcc, 0, v181, vcc
	v_add_co_u32_e32 v4, vcc, s59, v180
	s_nop 1
	v_addc_co_u32_e32 v5, vcc, 0, v181, vcc
	global_load_dwordx4 v[158:161], v[2:3], off sc0 nt
	global_load_dwordx4 v[142:145], v[4:5], off sc0 nt
	v_add_co_u32_e32 v2, vcc, s60, v180
	s_nop 1
	v_addc_co_u32_e32 v3, vcc, 0, v181, vcc
	v_add_co_u32_e32 v4, vcc, s61, v180
	s_nop 1
	v_addc_co_u32_e32 v5, vcc, 0, v181, vcc
	global_load_dwordx4 v[126:129], v[2:3], off sc0 nt
	global_load_dwordx4 v[130:133], v[4:5], off sc0 nt
	v_add_co_u32_e32 v2, vcc, s62, v180
	s_nop 1
	v_addc_co_u32_e32 v3, vcc, 0, v181, vcc
	v_add_co_u32_e32 v4, vcc, s63, v180
	s_nop 1
	v_addc_co_u32_e32 v5, vcc, 0, v181, vcc
	global_load_dwordx4 v[146:149], v[2:3], off sc0 nt
	global_load_dwordx4 v[50:53], v[4:5], off sc0 nt
	v_add_co_u32_e32 v2, vcc, s2, v180
	s_mov_b32 s2, 0xc24000
	s_nop 0
	v_addc_co_u32_e32 v3, vcc, 0, v181, vcc
	v_add_co_u32_e32 v4, vcc, s2, v180
	s_mov_b32 s2, 0xc28000
	s_nop 0
	v_addc_co_u32_e32 v5, vcc, 0, v181, vcc
	global_load_dwordx4 v[34:37], v[2:3], off sc0 nt
	global_load_dwordx4 v[42:45], v[4:5], off sc0 nt
	v_add_co_u32_e32 v2, vcc, s2, v180
	s_mov_b32 s2, 0xc2c000
	s_nop 0
	v_addc_co_u32_e32 v3, vcc, 0, v181, vcc
	v_add_co_u32_e32 v4, vcc, s2, v180
	s_mov_b32 s2, 0xc30000
	s_nop 0
	v_addc_co_u32_e32 v5, vcc, 0, v181, vcc
	global_load_dwordx4 v[134:137], v[2:3], off sc0 nt
	global_load_dwordx4 v[26:29], v[4:5], off sc0 nt
	v_add_co_u32_e32 v2, vcc, s2, v180
	s_mov_b32 s2, 0xc34000
	s_nop 0
	v_addc_co_u32_e32 v3, vcc, 0, v181, vcc
	v_add_co_u32_e32 v4, vcc, s2, v180
	s_mov_b32 s2, 0xc38000
	s_nop 0
	v_addc_co_u32_e32 v5, vcc, 0, v181, vcc
	global_load_dwordx4 v[10:13], v[2:3], off sc0 nt
	global_load_dwordx4 v[18:21], v[4:5], off sc0 nt
	v_add_co_u32_e32 v2, vcc, s2, v180
	s_mov_b32 s2, 0xc3c000
	s_nop 0
	v_addc_co_u32_e32 v3, vcc, 0, v181, vcc
	v_add_co_u32_e32 v4, vcc, s2, v180
	s_nop 1
	v_addc_co_u32_e32 v5, vcc, 0, v181, vcc
	global_load_dwordx4 v[54:57], v[2:3], off sc0 nt
	s_nop 0
	global_load_dwordx4 v[2:5], v[4:5], off sc0 nt
	ds_read_b128 v[6:9], v168 offset:34816
	ds_read_b128 v[14:17], v170 offset:34816
	ds_read_b128 v[22:25], v174 offset:34816
	ds_read_b128 v[30:33], v176 offset:34816
	s_waitcnt lgkmcnt(3)
	global_store_dwordx4 v[164:165], v[6:9], off offset:256 nt
	s_waitcnt lgkmcnt(2)
	global_store_dwordx4 v[166:167], v[14:17], off offset:256 nt
	s_waitcnt lgkmcnt(1)
	global_store_dwordx4 v[172:173], v[22:25], off offset:256 nt
	s_waitcnt lgkmcnt(0)
	global_store_dwordx4 v[178:179], v[30:33], off offset:256 nt
	s_waitcnt vmcnt(39)
	v_mul_f32_e32 v6, 0x43800000, v118
	s_waitcnt vmcnt(38)
	v_mul_f32_e32 v7, 0x43800000, v122
	v_med3_f32 v9, v6, s19, v1
	v_med3_f32 v7, v7, s19, v1
	v_mov_b32_e32 v6, v163
	v_cvt_pk_fp8_f32 v6, v9, v7
	s_waitcnt vmcnt(37)
	v_mul_f32_e32 v8, 0x43800000, v138
	s_waitcnt vmcnt(36)
	v_mul_f32_e32 v7, 0x43800000, v110
	v_med3_f32 v8, v8, s19, v1
	v_med3_f32 v7, v7, s19, v1
	v_cvt_pk_fp8_f32 v6, v8, v7 op_sel:[0,0,1]
	s_waitcnt vmcnt(35)
	v_mul_f32_e32 v7, 0x43800000, v98
	s_waitcnt vmcnt(34)
	v_mul_f32_e32 v8, 0x43800000, v102
	v_med3_f32 v14, v7, s19, v1
	v_med3_f32 v8, v8, s19, v1
	v_mov_b32_e32 v7, v163
	v_cvt_pk_fp8_f32 v7, v14, v8
	s_waitcnt vmcnt(33)
	v_mul_f32_e32 v9, 0x43800000, v114
	s_waitcnt vmcnt(32)
	v_mul_f32_e32 v8, 0x43800000, v90
	v_med3_f32 v9, v9, s19, v1
	v_med3_f32 v8, v8, s19, v1
	v_cvt_pk_fp8_f32 v7, v9, v8 op_sel:[0,0,1]
	s_waitcnt vmcnt(31)
	v_mul_f32_e32 v8, 0x43800000, v82
	s_waitcnt vmcnt(30)
	v_mul_f32_e32 v9, 0x43800000, v86
	v_med3_f32 v15, v8, s19, v1
	v_med3_f32 v9, v9, s19, v1
	v_mov_b32_e32 v8, v163
	v_cvt_pk_fp8_f32 v8, v15, v9
	s_waitcnt vmcnt(29)
	v_mul_f32_e32 v14, 0x43800000, v106
	s_waitcnt vmcnt(28)
	v_mul_f32_e32 v9, 0x43800000, v78
	v_med3_f32 v14, v14, s19, v1
	v_med3_f32 v9, v9, s19, v1
	v_cvt_pk_fp8_f32 v8, v14, v9 op_sel:[0,0,1]
	s_waitcnt vmcnt(27)
	v_mul_f32_e32 v9, 0x43800000, v70
	s_waitcnt vmcnt(26)
	v_mul_f32_e32 v14, 0x43800000, v74
	v_med3_f32 v16, v9, s19, v1
	v_med3_f32 v14, v14, s19, v1
	v_mov_b32_e32 v9, v163
	v_cvt_pk_fp8_f32 v9, v16, v14
	s_waitcnt vmcnt(25)
	v_mul_f32_e32 v15, 0x43800000, v94
	s_waitcnt vmcnt(24)
	v_mul_f32_e32 v14, 0x43800000, v66
	v_med3_f32 v15, v15, s19, v1
	v_med3_f32 v14, v14, s19, v1
	v_cvt_pk_fp8_f32 v9, v15, v14 op_sel:[0,0,1]
	v_mul_f32_e32 v14, 0x43800000, v119
	v_mul_f32_e32 v15, 0x43800000, v123
	v_med3_f32 v17, v14, s19, v1
	v_med3_f32 v15, v15, s19, v1
	v_mov_b32_e32 v14, v163
	v_cvt_pk_fp8_f32 v14, v17, v15
	v_mul_f32_e32 v16, 0x43800000, v139
	v_mul_f32_e32 v15, 0x43800000, v111
	v_med3_f32 v16, v16, s19, v1
	v_med3_f32 v15, v15, s19, v1
	v_cvt_pk_fp8_f32 v14, v16, v15 op_sel:[0,0,1]
	v_mul_f32_e32 v15, 0x43800000, v99
	v_mul_f32_e32 v16, 0x43800000, v103
	v_med3_f32 v22, v15, s19, v1
	v_med3_f32 v16, v16, s19, v1
	v_mov_b32_e32 v15, v163
	v_cvt_pk_fp8_f32 v15, v22, v16
	v_mul_f32_e32 v17, 0x43800000, v115
	v_mul_f32_e32 v16, 0x43800000, v91
	v_med3_f32 v17, v17, s19, v1
	v_med3_f32 v16, v16, s19, v1
	v_cvt_pk_fp8_f32 v15, v17, v16 op_sel:[0,0,1]
	v_mul_f32_e32 v16, 0x43800000, v83
	v_mul_f32_e32 v17, 0x43800000, v87
	v_med3_f32 v23, v16, s19, v1
	v_med3_f32 v17, v17, s19, v1
	v_mov_b32_e32 v16, v163
	v_cvt_pk_fp8_f32 v16, v23, v17
	v_mul_f32_e32 v22, 0x43800000, v107
	v_mul_f32_e32 v17, 0x43800000, v79
	v_med3_f32 v22, v22, s19, v1
	v_med3_f32 v17, v17, s19, v1
	v_cvt_pk_fp8_f32 v16, v22, v17 op_sel:[0,0,1]
	v_mul_f32_e32 v17, 0x43800000, v71
	v_mul_f32_e32 v22, 0x43800000, v75
	v_med3_f32 v24, v17, s19, v1
	v_med3_f32 v22, v22, s19, v1
	v_mov_b32_e32 v17, v163
	v_cvt_pk_fp8_f32 v17, v24, v22
	v_mul_f32_e32 v23, 0x43800000, v95
	v_mul_f32_e32 v22, 0x43800000, v67
	v_med3_f32 v23, v23, s19, v1
	v_med3_f32 v22, v22, s19, v1
	v_cvt_pk_fp8_f32 v17, v23, v22 op_sel:[0,0,1]
	v_mul_f32_e32 v22, 0x43800000, v120
	v_mul_f32_e32 v23, 0x43800000, v124
	v_med3_f32 v25, v22, s19, v1
	v_med3_f32 v23, v23, s19, v1
	v_mov_b32_e32 v22, v163
	v_cvt_pk_fp8_f32 v22, v25, v23
	v_mul_f32_e32 v24, 0x43800000, v140
	v_mul_f32_e32 v23, 0x43800000, v112
	v_med3_f32 v24, v24, s19, v1
	v_med3_f32 v23, v23, s19, v1
	v_cvt_pk_fp8_f32 v22, v24, v23 op_sel:[0,0,1]
	v_mul_f32_e32 v23, 0x43800000, v100
	v_mul_f32_e32 v24, 0x43800000, v104
	v_med3_f32 v30, v23, s19, v1
	v_med3_f32 v24, v24, s19, v1
	v_mov_b32_e32 v23, v163
	v_cvt_pk_fp8_f32 v23, v30, v24
	v_mul_f32_e32 v25, 0x43800000, v116
	v_mul_f32_e32 v24, 0x43800000, v92
	v_med3_f32 v25, v25, s19, v1
	v_med3_f32 v24, v24, s19, v1
	v_cvt_pk_fp8_f32 v23, v25, v24 op_sel:[0,0,1]
	v_mul_f32_e32 v24, 0x43800000, v84
	v_mul_f32_e32 v25, 0x43800000, v88
	v_med3_f32 v31, v24, s19, v1
	v_med3_f32 v25, v25, s19, v1
	v_mov_b32_e32 v24, v163
	v_cvt_pk_fp8_f32 v24, v31, v25
	v_mul_f32_e32 v30, 0x43800000, v108
	v_mul_f32_e32 v25, 0x43800000, v80
	v_med3_f32 v30, v30, s19, v1
	v_med3_f32 v25, v25, s19, v1
	v_cvt_pk_fp8_f32 v24, v30, v25 op_sel:[0,0,1]
	v_mul_f32_e32 v25, 0x43800000, v72
	v_mul_f32_e32 v30, 0x43800000, v76
	v_med3_f32 v32, v25, s19, v1
	v_med3_f32 v30, v30, s19, v1
	v_mov_b32_e32 v25, v163
	v_cvt_pk_fp8_f32 v25, v32, v30
	v_mul_f32_e32 v31, 0x43800000, v96
	v_mul_f32_e32 v30, 0x43800000, v68
	v_med3_f32 v31, v31, s19, v1
	v_med3_f32 v30, v30, s19, v1
	v_cvt_pk_fp8_f32 v25, v31, v30 op_sel:[0,0,1]
	v_mul_f32_e32 v30, 0x43800000, v121
	v_mul_f32_e32 v31, 0x43800000, v125
	v_med3_f32 v33, v30, s19, v1
	v_med3_f32 v31, v31, s19, v1
	v_mov_b32_e32 v30, v163
	v_cvt_pk_fp8_f32 v30, v33, v31
	v_mul_f32_e32 v32, 0x43800000, v141
	v_mul_f32_e32 v31, 0x43800000, v113
	v_med3_f32 v32, v32, s19, v1
	v_med3_f32 v31, v31, s19, v1
	v_cvt_pk_fp8_f32 v30, v32, v31 op_sel:[0,0,1]
	v_mul_f32_e32 v31, 0x43800000, v101
	v_mul_f32_e32 v32, 0x43800000, v105
	v_med3_f32 v38, v31, s19, v1
	v_med3_f32 v32, v32, s19, v1
	v_mov_b32_e32 v31, v163
	v_cvt_pk_fp8_f32 v31, v38, v32
	v_mul_f32_e32 v33, 0x43800000, v117
	v_mul_f32_e32 v32, 0x43800000, v93
	v_med3_f32 v33, v33, s19, v1
	v_med3_f32 v32, v32, s19, v1
	v_cvt_pk_fp8_f32 v31, v33, v32 op_sel:[0,0,1]
	v_mul_f32_e32 v32, 0x43800000, v85
	v_mul_f32_e32 v33, 0x43800000, v89
	v_med3_f32 v39, v32, s19, v1
	v_med3_f32 v33, v33, s19, v1
	v_mov_b32_e32 v32, v163
	v_cvt_pk_fp8_f32 v32, v39, v33
	v_mul_f32_e32 v38, 0x43800000, v109
	v_mul_f32_e32 v33, 0x43800000, v81
	v_med3_f32 v38, v38, s19, v1
	v_med3_f32 v33, v33, s19, v1
	v_cvt_pk_fp8_f32 v32, v38, v33 op_sel:[0,0,1]
	v_mul_f32_e32 v33, 0x43800000, v73
	v_mul_f32_e32 v38, 0x43800000, v77
	v_med3_f32 v40, v33, s19, v1
	v_med3_f32 v38, v38, s19, v1
	v_mov_b32_e32 v33, v163
	v_cvt_pk_fp8_f32 v33, v40, v38
	v_mul_f32_e32 v39, 0x43800000, v97
	v_mul_f32_e32 v38, 0x43800000, v69
	v_med3_f32 v39, v39, s19, v1
	v_med3_f32 v38, v38, s19, v1
	v_cvt_pk_fp8_f32 v33, v39, v38 op_sel:[0,0,1]
	ds_write_b128 v182, v[6:9]
	ds_write_b128 v182, v[14:17] offset:272
	ds_write_b128 v182, v[22:25] offset:544
	ds_write_b128 v182, v[30:33] offset:816
	s_waitcnt lgkmcnt(0)
	s_barrier
	s_mov_b32 s2, 0x1000000
	v_add_co_u32_e32 v6, vcc, s2, v180
	s_mov_b32 s2, 0x1004000
	s_nop 0
	v_addc_co_u32_e32 v7, vcc, 0, v181, vcc
	v_add_co_u32_e32 v8, vcc, s2, v180
	s_mov_b32 s2, 0x1008000
	s_nop 0
	v_addc_co_u32_e32 v9, vcc, 0, v181, vcc
	global_load_dwordx4 v[98:101], v[6:7], off sc0 nt
	global_load_dwordx4 v[106:109], v[8:9], off sc0 nt
	v_add_co_u32_e32 v6, vcc, s2, v180
	s_mov_b32 s2, 0x100c000
	s_nop 0
	v_addc_co_u32_e32 v7, vcc, 0, v181, vcc
	v_add_co_u32_e32 v8, vcc, s2, v180
	s_mov_b32 s2, 0x1010000
	s_nop 0
	v_addc_co_u32_e32 v9, vcc, 0, v181, vcc
	global_load_dwordx4 v[122:125], v[6:7], off sc0 nt
	global_load_dwordx4 v[82:85], v[8:9], off sc0 nt
	v_add_co_u32_e32 v6, vcc, s2, v180
	s_mov_b32 s2, 0x1014000
	s_nop 0
	v_addc_co_u32_e32 v7, vcc, 0, v181, vcc
	v_add_co_u32_e32 v8, vcc, s2, v180
	s_mov_b32 s2, 0x1018000
	s_nop 0
	v_addc_co_u32_e32 v9, vcc, 0, v181, vcc
	global_load_dwordx4 v[66:69], v[6:7], off sc0 nt
	global_load_dwordx4 v[74:77], v[8:9], off sc0 nt
	v_add_co_u32_e32 v6, vcc, s2, v180
	s_mov_b32 s2, 0x101c000
	s_nop 0
	v_addc_co_u32_e32 v7, vcc, 0, v181, vcc
	v_add_co_u32_e32 v8, vcc, s2, v180
	s_mov_b32 s2, 0x1020000
	s_nop 0
	v_addc_co_u32_e32 v9, vcc, 0, v181, vcc
	global_load_dwordx4 v[114:117], v[6:7], off sc0 nt
	global_load_dwordx4 v[58:61], v[8:9], off sc0 nt
	v_add_co_u32_e32 v6, vcc, s2, v180
	s_mov_b32 s2, 0x1024000
	s_nop 0
	v_addc_co_u32_e32 v7, vcc, 0, v181, vcc
	v_add_co_u32_e32 v8, vcc, s2, v180
	s_mov_b32 s2, 0x1028000
	s_nop 0
	v_addc_co_u32_e32 v9, vcc, 0, v181, vcc
	global_load_dwordx4 v[38:41], v[6:7], off sc0 nt
	global_load_dwordx4 v[46:49], v[8:9], off sc0 nt
	v_add_co_u32_e32 v6, vcc, s2, v180
	s_mov_b32 s2, 0x102c000
	s_nop 0
	v_addc_co_u32_e32 v7, vcc, 0, v181, vcc
	v_add_co_u32_e32 v8, vcc, s2, v180
	s_mov_b32 s2, 0x1030000
	s_nop 0
	v_addc_co_u32_e32 v9, vcc, 0, v181, vcc
	global_load_dwordx4 v[86:89], v[6:7], off sc0 nt
	global_load_dwordx4 v[30:33], v[8:9], off sc0 nt
	v_add_co_u32_e32 v6, vcc, s2, v180
	s_mov_b32 s2, 0x1034000
	s_nop 0
	v_addc_co_u32_e32 v7, vcc, 0, v181, vcc
	v_add_co_u32_e32 v8, vcc, s2, v180
	s_mov_b32 s2, 0x1038000
	s_nop 0
	v_addc_co_u32_e32 v9, vcc, 0, v181, vcc
	global_load_dwordx4 v[14:17], v[6:7], off sc0 nt
	global_load_dwordx4 v[22:25], v[8:9], off sc0 nt
	v_add_co_u32_e32 v6, vcc, s2, v180
	s_mov_b32 s2, 0x103c000
	s_nop 0
	v_addc_co_u32_e32 v7, vcc, 0, v181, vcc
	v_add_co_u32_e32 v8, vcc, s2, v180
	s_nop 1
	v_addc_co_u32_e32 v9, vcc, 0, v181, vcc
	global_load_dwordx4 v[62:65], v[6:7], off sc0 nt
	s_nop 0
	global_load_dwordx4 v[6:9], v[8:9], off sc0 nt
	ds_read_b128 v[70:73], v168
	ds_read_b128 v[78:81], v170
	ds_read_b128 v[90:93], v174
	ds_read_b128 v[94:97], v176
	s_waitcnt lgkmcnt(3)
	global_store_dwordx4 v[164:165], v[70:73], off offset:512 nt
	s_waitcnt lgkmcnt(2)
	global_store_dwordx4 v[166:167], v[78:81], off offset:512 nt
	s_waitcnt lgkmcnt(1)
	global_store_dwordx4 v[172:173], v[90:93], off offset:512 nt
	s_waitcnt lgkmcnt(0)
	global_store_dwordx4 v[178:179], v[94:97], off offset:512 nt
	s_waitcnt vmcnt(39)
	v_mul_f32_e32 v70, 0x43800000, v150
	s_waitcnt vmcnt(38)
	v_mul_f32_e32 v71, 0x43800000, v154
	v_med3_f32 v73, v70, s19, v1
	v_med3_f32 v71, v71, s19, v1
	v_mov_b32_e32 v70, v163
	v_cvt_pk_fp8_f32 v70, v73, v71
	s_waitcnt vmcnt(37)
	v_mul_f32_e32 v72, 0x43800000, v158
	s_waitcnt vmcnt(36)
	v_mul_f32_e32 v71, 0x43800000, v142
	v_med3_f32 v72, v72, s19, v1
	v_med3_f32 v71, v71, s19, v1
	v_cvt_pk_fp8_f32 v70, v72, v71 op_sel:[0,0,1]
	s_waitcnt vmcnt(35)
	v_mul_f32_e32 v71, 0x43800000, v126
	s_waitcnt vmcnt(34)
	v_mul_f32_e32 v72, 0x43800000, v130
	v_med3_f32 v78, v71, s19, v1
	v_med3_f32 v72, v72, s19, v1
	v_mov_b32_e32 v71, v163
	v_cvt_pk_fp8_f32 v71, v78, v72
	s_waitcnt vmcnt(33)
	v_mul_f32_e32 v73, 0x43800000, v146
	s_waitcnt vmcnt(32)
	v_mul_f32_e32 v50, 0x43800000, v50
	v_med3_f32 v72, v73, s19, v1
	v_med3_f32 v50, v50, s19, v1
	s_waitcnt vmcnt(31)
	v_mul_f32_e32 v34, 0x43800000, v34
	s_waitcnt vmcnt(30)
	v_mul_f32_e32 v42, 0x43800000, v42
	v_cvt_pk_fp8_f32 v71, v72, v50 op_sel:[0,0,1]
	v_med3_f32 v34, v34, s19, v1
	v_med3_f32 v42, v42, s19, v1
	v_mov_b32_e32 v72, v163
	v_cvt_pk_fp8_f32 v72, v34, v42
	s_waitcnt vmcnt(27)
	v_mul_f32_e32 v10, 0x43800000, v10
	s_waitcnt vmcnt(26)
	v_mul_f32_e32 v18, 0x43800000, v18
	v_med3_f32 v10, v10, s19, v1
	v_med3_f32 v18, v18, s19, v1
	v_mov_b32_e32 v73, v163
	v_mul_f32_e32 v50, 0x43800000, v134
	v_mul_f32_e32 v26, 0x43800000, v26
	v_cvt_pk_fp8_f32 v73, v10, v18
	v_med3_f32 v34, v50, s19, v1
	v_med3_f32 v26, v26, s19, v1
	v_cvt_pk_fp8_f32 v72, v34, v26 op_sel:[0,0,1]
	s_waitcnt vmcnt(25)
	v_mul_f32_e32 v26, 0x43800000, v54
	s_waitcnt vmcnt(24)
	v_mul_f32_e32 v2, 0x43800000, v2
	v_med3_f32 v10, v26, s19, v1
	v_med3_f32 v2, v2, s19, v1
	v_cvt_pk_fp8_f32 v73, v10, v2 op_sel:[0,0,1]
	v_mul_f32_e32 v2, 0x43800000, v151
	v_mul_f32_e32 v10, 0x43800000, v155
	v_med3_f32 v2, v2, s19, v1
	v_med3_f32 v10, v10, s19, v1
	v_mov_b32_e32 v78, v163
	v_cvt_pk_fp8_f32 v78, v2, v10
	v_mul_f32_e32 v18, 0x43800000, v159
	v_mul_f32_e32 v2, 0x43800000, v143
	v_med3_f32 v10, v18, s19, v1
	v_med3_f32 v2, v2, s19, v1
	v_cvt_pk_fp8_f32 v78, v10, v2 op_sel:[0,0,1]
	v_mul_f32_e32 v2, 0x43800000, v127
	v_mul_f32_e32 v10, 0x43800000, v131
	v_med3_f32 v2, v2, s19, v1
	v_med3_f32 v10, v10, s19, v1
	v_mov_b32_e32 v79, v163
	v_cvt_pk_fp8_f32 v79, v2, v10
	v_mul_f32_e32 v18, 0x43800000, v147
	v_mul_f32_e32 v2, 0x43800000, v51
	v_med3_f32 v10, v18, s19, v1
	v_med3_f32 v2, v2, s19, v1
	v_cvt_pk_fp8_f32 v79, v10, v2 op_sel:[0,0,1]
	v_mul_f32_e32 v2, 0x43800000, v35
	v_mul_f32_e32 v10, 0x43800000, v43
	v_med3_f32 v2, v2, s19, v1
	v_med3_f32 v10, v10, s19, v1
	v_mov_b32_e32 v80, v163
	v_cvt_pk_fp8_f32 v80, v2, v10
	v_mul_f32_e32 v18, 0x43800000, v135
	v_mul_f32_e32 v2, 0x43800000, v27
	v_med3_f32 v10, v18, s19, v1
	v_med3_f32 v2, v2, s19, v1
	v_cvt_pk_fp8_f32 v80, v10, v2 op_sel:[0,0,1]
	v_mul_f32_e32 v2, 0x43800000, v11
	v_mul_f32_e32 v10, 0x43800000, v19
	v_med3_f32 v2, v2, s19, v1
	v_med3_f32 v10, v10, s19, v1
	v_mov_b32_e32 v81, v163
	v_cvt_pk_fp8_f32 v81, v2, v10
	v_mul_f32_e32 v11, 0x43800000, v55
	v_mul_f32_e32 v2, 0x43800000, v3
	v_med3_f32 v3, v11, s19, v1
	v_med3_f32 v2, v2, s19, v1
	v_cvt_pk_fp8_f32 v81, v3, v2 op_sel:[0,0,1]
	v_mul_f32_e32 v2, 0x43800000, v152
	v_mul_f32_e32 v3, 0x43800000, v156
	v_med3_f32 v2, v2, s19, v1
	v_med3_f32 v3, v3, s19, v1
	v_mov_b32_e32 v90, v163
	v_cvt_pk_fp8_f32 v90, v2, v3
	v_mul_f32_e32 v10, 0x43800000, v160
	v_mul_f32_e32 v2, 0x43800000, v144
	v_med3_f32 v3, v10, s19, v1
	v_med3_f32 v2, v2, s19, v1
	v_cvt_pk_fp8_f32 v90, v3, v2 op_sel:[0,0,1]
	v_mul_f32_e32 v2, 0x43800000, v128
	v_mul_f32_e32 v3, 0x43800000, v132
	v_med3_f32 v2, v2, s19, v1
	v_med3_f32 v3, v3, s19, v1
	v_mov_b32_e32 v91, v163
	v_cvt_pk_fp8_f32 v91, v2, v3
	v_mul_f32_e32 v10, 0x43800000, v148
	v_mul_f32_e32 v2, 0x43800000, v52
	v_med3_f32 v3, v10, s19, v1
	v_med3_f32 v2, v2, s19, v1
	v_cvt_pk_fp8_f32 v91, v3, v2 op_sel:[0,0,1]
	v_mul_f32_e32 v2, 0x43800000, v36
	v_mul_f32_e32 v3, 0x43800000, v44
	v_med3_f32 v2, v2, s19, v1
	v_med3_f32 v3, v3, s19, v1
	v_mov_b32_e32 v92, v163
	v_cvt_pk_fp8_f32 v92, v2, v3
	v_mul_f32_e32 v10, 0x43800000, v136
	v_mul_f32_e32 v2, 0x43800000, v28
	v_med3_f32 v3, v10, s19, v1
	v_med3_f32 v2, v2, s19, v1
	v_cvt_pk_fp8_f32 v92, v3, v2 op_sel:[0,0,1]
	v_mul_f32_e32 v2, 0x43800000, v12
	v_mul_f32_e32 v3, 0x43800000, v20
	v_med3_f32 v2, v2, s19, v1
	v_med3_f32 v3, v3, s19, v1
	v_mov_b32_e32 v93, v163
	v_cvt_pk_fp8_f32 v93, v2, v3
	v_mul_f32_e32 v10, 0x43800000, v56
	v_mul_f32_e32 v2, 0x43800000, v4
	v_med3_f32 v3, v10, s19, v1
	v_med3_f32 v2, v2, s19, v1
	v_cvt_pk_fp8_f32 v93, v3, v2 op_sel:[0,0,1]
	v_mul_f32_e32 v2, 0x43800000, v153
	v_mul_f32_e32 v3, 0x43800000, v157
	v_med3_f32 v2, v2, s19, v1
	v_med3_f32 v3, v3, s19, v1
	v_mov_b32_e32 v10, v163
	v_cvt_pk_fp8_f32 v10, v2, v3
	v_mul_f32_e32 v4, 0x43800000, v161
	v_mul_f32_e32 v2, 0x43800000, v145
	v_med3_f32 v3, v4, s19, v1
	v_med3_f32 v2, v2, s19, v1
	v_cvt_pk_fp8_f32 v10, v3, v2 op_sel:[0,0,1]
	v_mul_f32_e32 v2, 0x43800000, v129
	v_mul_f32_e32 v3, 0x43800000, v133
	v_med3_f32 v2, v2, s19, v1
	v_med3_f32 v3, v3, s19, v1
	v_mov_b32_e32 v11, v163
	v_cvt_pk_fp8_f32 v11, v2, v3
	v_mul_f32_e32 v4, 0x43800000, v149
	v_mul_f32_e32 v2, 0x43800000, v53
	v_med3_f32 v3, v4, s19, v1
	v_med3_f32 v2, v2, s19, v1
	v_cvt_pk_fp8_f32 v11, v3, v2 op_sel:[0,0,1]
	v_mul_f32_e32 v2, 0x43800000, v37
	v_mul_f32_e32 v3, 0x43800000, v45
	v_med3_f32 v2, v2, s19, v1
	v_med3_f32 v3, v3, s19, v1
	v_mov_b32_e32 v12, v163
	v_cvt_pk_fp8_f32 v12, v2, v3
	v_mul_f32_e32 v4, 0x43800000, v137
	v_mul_f32_e32 v2, 0x43800000, v29
	v_med3_f32 v3, v4, s19, v1
	v_med3_f32 v2, v2, s19, v1
	v_cvt_pk_fp8_f32 v12, v3, v2 op_sel:[0,0,1]
	v_mul_f32_e32 v2, 0x43800000, v13
	v_mul_f32_e32 v3, 0x43800000, v21
	v_med3_f32 v2, v2, s19, v1
	v_med3_f32 v3, v3, s19, v1
	v_mov_b32_e32 v13, v163
	v_cvt_pk_fp8_f32 v13, v2, v3
	v_mul_f32_e32 v4, 0x43800000, v57
	v_mul_f32_e32 v2, 0x43800000, v5
	v_med3_f32 v3, v4, s19, v1
	v_med3_f32 v2, v2, s19, v1
	v_cvt_pk_fp8_f32 v13, v3, v2 op_sel:[0,0,1]
	ds_write_b128 v182, v[70:73] offset:34816
	ds_write_b128 v182, v[78:81] offset:35088
	ds_write_b128 v182, v[90:93] offset:35360
	ds_write_b128 v182, v[10:13] offset:35632
	s_waitcnt lgkmcnt(0)
	s_barrier
	s_mov_b32 s2, 0x1400000
	v_add_co_u32_e32 v2, vcc, s2, v180
	s_mov_b32 s2, 0x1404000
	s_nop 0
	v_addc_co_u32_e32 v3, vcc, 0, v181, vcc
	v_add_co_u32_e32 v4, vcc, s2, v180
	s_mov_b32 s2, 0x1408000
	s_nop 0
	v_addc_co_u32_e32 v5, vcc, 0, v181, vcc
	global_load_dwordx4 v[102:105], v[2:3], off sc0 nt
	global_load_dwordx4 v[110:113], v[4:5], off sc0 nt
	v_add_co_u32_e32 v2, vcc, s2, v180
	s_mov_b32 s2, 0x140c000
	s_nop 0
	v_addc_co_u32_e32 v3, vcc, 0, v181, vcc
	v_add_co_u32_e32 v4, vcc, s2, v180
	s_mov_b32 s2, 0x1410000
	s_nop 0
	v_addc_co_u32_e32 v5, vcc, 0, v181, vcc
	global_load_dwordx4 v[126:129], v[2:3], off sc0 nt
	global_load_dwordx4 v[90:93], v[4:5], off sc0 nt
	v_add_co_u32_e32 v2, vcc, s2, v180
	s_mov_b32 s2, 0x1414000
	s_nop 0
	v_addc_co_u32_e32 v3, vcc, 0, v181, vcc
	v_add_co_u32_e32 v4, vcc, s2, v180
	s_mov_b32 s2, 0x1418000
	s_nop 0
	v_addc_co_u32_e32 v5, vcc, 0, v181, vcc
	global_load_dwordx4 v[70:73], v[2:3], off sc0 nt
	global_load_dwordx4 v[78:81], v[4:5], off sc0 nt
	v_add_co_u32_e32 v2, vcc, s2, v180
	s_mov_b32 s2, 0x141c000
	s_nop 0
	v_addc_co_u32_e32 v3, vcc, 0, v181, vcc
	v_add_co_u32_e32 v4, vcc, s2, v180
	s_mov_b32 s2, 0x1420000
	s_nop 0
	v_addc_co_u32_e32 v5, vcc, 0, v181, vcc
	global_load_dwordx4 v[118:121], v[2:3], off sc0 nt
	global_load_dwordx4 v[50:53], v[4:5], off sc0 nt
	v_add_co_u32_e32 v2, vcc, s2, v180
	s_mov_b32 s2, 0x1424000
	s_nop 0
	v_addc_co_u32_e32 v3, vcc, 0, v181, vcc
	v_add_co_u32_e32 v4, vcc, s2, v180
	s_mov_b32 s2, 0x1428000
	s_nop 0
	v_addc_co_u32_e32 v5, vcc, 0, v181, vcc
	global_load_dwordx4 v[34:37], v[2:3], off sc0 nt
	global_load_dwordx4 v[42:45], v[4:5], off sc0 nt
	v_add_co_u32_e32 v2, vcc, s2, v180
	s_mov_b32 s2, 0x142c000
	s_nop 0
	v_addc_co_u32_e32 v3, vcc, 0, v181, vcc
	v_add_co_u32_e32 v4, vcc, s2, v180
	s_mov_b32 s2, 0x1430000
	s_nop 0
	v_addc_co_u32_e32 v5, vcc, 0, v181, vcc
	global_load_dwordx4 v[94:97], v[2:3], off sc0 nt
	global_load_dwordx4 v[26:29], v[4:5], off sc0 nt
	v_add_co_u32_e32 v2, vcc, s2, v180
	s_mov_b32 s2, 0x1434000
	s_nop 0
	v_addc_co_u32_e32 v3, vcc, 0, v181, vcc
	v_add_co_u32_e32 v4, vcc, s2, v180
	s_mov_b32 s2, 0x1438000
	s_nop 0
	v_addc_co_u32_e32 v5, vcc, 0, v181, vcc
	global_load_dwordx4 v[10:13], v[2:3], off sc0 nt
	global_load_dwordx4 v[18:21], v[4:5], off sc0 nt
	v_add_co_u32_e32 v2, vcc, s2, v180
	s_mov_b32 s2, 0x143c000
	s_nop 0
	v_addc_co_u32_e32 v3, vcc, 0, v181, vcc
	v_add_co_u32_e32 v4, vcc, s2, v180
	s_nop 1
	v_addc_co_u32_e32 v5, vcc, 0, v181, vcc
	global_load_dwordx4 v[54:57], v[2:3], off sc0 nt
	s_nop 0
	global_load_dwordx4 v[2:5], v[4:5], off sc0 nt
	ds_read_b128 v[130:133], v168 offset:34816
	ds_read_b128 v[134:137], v170 offset:34816
	ds_read_b128 v[138:141], v174 offset:34816
	ds_read_b128 v[142:145], v176 offset:34816
	s_waitcnt lgkmcnt(3)
	global_store_dwordx4 v[164:165], v[130:133], off offset:768 nt
	s_waitcnt lgkmcnt(2)
	global_store_dwordx4 v[166:167], v[134:137], off offset:768 nt
	s_waitcnt lgkmcnt(1)
	global_store_dwordx4 v[172:173], v[138:141], off offset:768 nt
	s_waitcnt lgkmcnt(0)
	global_store_dwordx4 v[178:179], v[142:145], off offset:768 nt
	s_waitcnt vmcnt(39)
	v_mul_f32_e32 v98, 0x43800000, v98
	s_waitcnt vmcnt(38)
	v_mul_f32_e32 v106, 0x43800000, v106
	v_med3_f32 v98, v98, s19, v1
	v_med3_f32 v106, v106, s19, v1
	v_mov_b32_e32 v130, v163
	v_cvt_pk_fp8_f32 v130, v98, v106
	s_waitcnt vmcnt(35)
	v_mul_f32_e32 v66, 0x43800000, v66
	s_waitcnt vmcnt(34)
	v_mul_f32_e32 v74, 0x43800000, v74
	v_med3_f32 v66, v66, s19, v1
	v_med3_f32 v74, v74, s19, v1
	v_mov_b32_e32 v131, v163
	v_mul_f32_e32 v122, 0x43800000, v122
	v_mul_f32_e32 v82, 0x43800000, v82
	v_cvt_pk_fp8_f32 v131, v66, v74
	s_waitcnt vmcnt(31)
	v_mul_f32_e32 v38, 0x43800000, v38
	s_waitcnt vmcnt(30)
	v_mul_f32_e32 v46, 0x43800000, v46
	v_med3_f32 v98, v122, s19, v1
	v_med3_f32 v82, v82, s19, v1
	v_med3_f32 v38, v38, s19, v1
	v_med3_f32 v46, v46, s19, v1
	v_mov_b32_e32 v132, v163
	v_cvt_pk_fp8_f32 v130, v98, v82 op_sel:[0,0,1]
	v_mul_f32_e32 v82, 0x43800000, v114
	v_mul_f32_e32 v58, 0x43800000, v58
	v_cvt_pk_fp8_f32 v132, v38, v46
	s_waitcnt vmcnt(27)
	v_mul_f32_e32 v14, 0x43800000, v14
	s_waitcnt vmcnt(26)
	v_mul_f32_e32 v22, 0x43800000, v22
	v_med3_f32 v66, v82, s19, v1
	v_med3_f32 v58, v58, s19, v1
	v_med3_f32 v14, v14, s19, v1
	v_med3_f32 v22, v22, s19, v1
	v_mov_b32_e32 v133, v163
	v_cvt_pk_fp8_f32 v131, v66, v58 op_sel:[0,0,1]
	v_mul_f32_e32 v58, 0x43800000, v86
	v_mul_f32_e32 v30, 0x43800000, v30
	v_cvt_pk_fp8_f32 v133, v14, v22
	v_med3_f32 v38, v58, s19, v1
	v_med3_f32 v30, v30, s19, v1
	v_cvt_pk_fp8_f32 v132, v38, v30 op_sel:[0,0,1]
	s_waitcnt vmcnt(25)
	v_mul_f32_e32 v30, 0x43800000, v62
	s_waitcnt vmcnt(24)
	v_mul_f32_e32 v6, 0x43800000, v6
	v_med3_f32 v14, v30, s19, v1
	v_med3_f32 v6, v6, s19, v1
	v_cvt_pk_fp8_f32 v133, v14, v6 op_sel:[0,0,1]
	v_mul_f32_e32 v6, 0x43800000, v99
	v_mul_f32_e32 v14, 0x43800000, v107
	v_med3_f32 v6, v6, s19, v1
	v_med3_f32 v14, v14, s19, v1
	v_mov_b32_e32 v134, v163
	v_cvt_pk_fp8_f32 v134, v6, v14
	v_mul_f32_e32 v22, 0x43800000, v123
	v_mul_f32_e32 v6, 0x43800000, v83
	v_med3_f32 v14, v22, s19, v1
	v_med3_f32 v6, v6, s19, v1
	v_cvt_pk_fp8_f32 v134, v14, v6 op_sel:[0,0,1]
	v_mul_f32_e32 v6, 0x43800000, v67
	v_mul_f32_e32 v14, 0x43800000, v75
	v_med3_f32 v6, v6, s19, v1
	v_med3_f32 v14, v14, s19, v1
	v_mov_b32_e32 v135, v163
	v_cvt_pk_fp8_f32 v135, v6, v14
	v_mul_f32_e32 v22, 0x43800000, v115
	v_mul_f32_e32 v6, 0x43800000, v59
	v_med3_f32 v14, v22, s19, v1
	v_med3_f32 v6, v6, s19, v1
	v_cvt_pk_fp8_f32 v135, v14, v6 op_sel:[0,0,1]
	v_mul_f32_e32 v6, 0x43800000, v39
	v_mul_f32_e32 v14, 0x43800000, v47
	v_med3_f32 v6, v6, s19, v1
	v_med3_f32 v14, v14, s19, v1
	v_mov_b32_e32 v136, v163
	v_cvt_pk_fp8_f32 v136, v6, v14
	v_mul_f32_e32 v22, 0x43800000, v87
	v_mul_f32_e32 v6, 0x43800000, v31
	v_med3_f32 v14, v22, s19, v1
	v_med3_f32 v6, v6, s19, v1
	v_cvt_pk_fp8_f32 v136, v14, v6 op_sel:[0,0,1]
	v_mul_f32_e32 v6, 0x43800000, v15
	v_mul_f32_e32 v14, 0x43800000, v23
	v_med3_f32 v6, v6, s19, v1
	v_med3_f32 v14, v14, s19, v1
	v_mov_b32_e32 v137, v163
	v_cvt_pk_fp8_f32 v137, v6, v14
	v_mul_f32_e32 v15, 0x43800000, v63
	v_mul_f32_e32 v6, 0x43800000, v7
	v_med3_f32 v7, v15, s19, v1
	v_med3_f32 v6, v6, s19, v1
	v_cvt_pk_fp8_f32 v137, v7, v6 op_sel:[0,0,1]
	v_mul_f32_e32 v6, 0x43800000, v100
	v_mul_f32_e32 v7, 0x43800000, v108
	v_med3_f32 v6, v6, s19, v1
	v_med3_f32 v7, v7, s19, v1
	v_mov_b32_e32 v138, v163
	v_cvt_pk_fp8_f32 v138, v6, v7
	v_mul_f32_e32 v14, 0x43800000, v124
	v_mul_f32_e32 v6, 0x43800000, v84
	v_med3_f32 v7, v14, s19, v1
	v_med3_f32 v6, v6, s19, v1
	v_cvt_pk_fp8_f32 v138, v7, v6 op_sel:[0,0,1]
	v_mul_f32_e32 v6, 0x43800000, v68
	v_mul_f32_e32 v7, 0x43800000, v76
	v_med3_f32 v6, v6, s19, v1
	v_med3_f32 v7, v7, s19, v1
	v_mov_b32_e32 v139, v163
	v_cvt_pk_fp8_f32 v139, v6, v7
	v_mul_f32_e32 v14, 0x43800000, v116
	v_mul_f32_e32 v6, 0x43800000, v60
	v_med3_f32 v7, v14, s19, v1
	v_med3_f32 v6, v6, s19, v1
	v_cvt_pk_fp8_f32 v139, v7, v6 op_sel:[0,0,1]
	v_mul_f32_e32 v6, 0x43800000, v40
	v_mul_f32_e32 v7, 0x43800000, v48
	v_med3_f32 v6, v6, s19, v1
	v_med3_f32 v7, v7, s19, v1
	v_mov_b32_e32 v140, v163
	v_cvt_pk_fp8_f32 v140, v6, v7
	v_mul_f32_e32 v14, 0x43800000, v88
	v_mul_f32_e32 v6, 0x43800000, v32
	v_med3_f32 v7, v14, s19, v1
	v_med3_f32 v6, v6, s19, v1
	v_cvt_pk_fp8_f32 v140, v7, v6 op_sel:[0,0,1]
	v_mul_f32_e32 v6, 0x43800000, v16
	v_mul_f32_e32 v7, 0x43800000, v24
	v_med3_f32 v6, v6, s19, v1
	v_med3_f32 v7, v7, s19, v1
	v_mov_b32_e32 v141, v163
	v_cvt_pk_fp8_f32 v141, v6, v7
	v_mul_f32_e32 v14, 0x43800000, v64
	v_mul_f32_e32 v6, 0x43800000, v8
	v_med3_f32 v7, v14, s19, v1
	v_med3_f32 v6, v6, s19, v1
	v_cvt_pk_fp8_f32 v141, v7, v6 op_sel:[0,0,1]
	v_mul_f32_e32 v6, 0x43800000, v101
	v_mul_f32_e32 v7, 0x43800000, v109
	v_med3_f32 v6, v6, s19, v1
	v_med3_f32 v7, v7, s19, v1
	v_mov_b32_e32 v14, v163
	v_cvt_pk_fp8_f32 v14, v6, v7
	v_mul_f32_e32 v8, 0x43800000, v125
	v_mul_f32_e32 v6, 0x43800000, v85
	v_med3_f32 v7, v8, s19, v1
	v_med3_f32 v6, v6, s19, v1
	v_cvt_pk_fp8_f32 v14, v7, v6 op_sel:[0,0,1]
	v_mul_f32_e32 v6, 0x43800000, v69
	v_mul_f32_e32 v7, 0x43800000, v77
	v_med3_f32 v6, v6, s19, v1
	v_med3_f32 v7, v7, s19, v1
	v_mov_b32_e32 v15, v163
	v_cvt_pk_fp8_f32 v15, v6, v7
	v_mul_f32_e32 v8, 0x43800000, v117
	v_mul_f32_e32 v6, 0x43800000, v61
	v_med3_f32 v7, v8, s19, v1
	v_med3_f32 v6, v6, s19, v1
	v_cvt_pk_fp8_f32 v15, v7, v6 op_sel:[0,0,1]
	v_mul_f32_e32 v6, 0x43800000, v41
	v_mul_f32_e32 v7, 0x43800000, v49
	v_med3_f32 v6, v6, s19, v1
	v_med3_f32 v7, v7, s19, v1
	v_mov_b32_e32 v16, v163
	v_cvt_pk_fp8_f32 v16, v6, v7
	v_mul_f32_e32 v8, 0x43800000, v89
	v_mul_f32_e32 v6, 0x43800000, v33
	v_med3_f32 v7, v8, s19, v1
	v_med3_f32 v6, v6, s19, v1
	v_cvt_pk_fp8_f32 v16, v7, v6 op_sel:[0,0,1]
	v_mul_f32_e32 v6, 0x43800000, v17
	v_mul_f32_e32 v7, 0x43800000, v25
	v_med3_f32 v6, v6, s19, v1
	v_med3_f32 v7, v7, s19, v1
	v_mov_b32_e32 v17, v163
	v_cvt_pk_fp8_f32 v17, v6, v7
	v_mul_f32_e32 v8, 0x43800000, v65
	v_mul_f32_e32 v6, 0x43800000, v9
	v_med3_f32 v7, v8, s19, v1
	v_med3_f32 v6, v6, s19, v1
	v_cvt_pk_fp8_f32 v17, v7, v6 op_sel:[0,0,1]
	ds_write_b128 v182, v[130:133]
	ds_write_b128 v182, v[134:137] offset:272
	ds_write_b128 v182, v[138:141] offset:544
	ds_write_b128 v182, v[14:17] offset:816
	s_waitcnt lgkmcnt(0)
	s_barrier
	s_mov_b32 s2, 0x1800000
	v_add_co_u32_e32 v6, vcc, s2, v180
	s_mov_b32 s2, 0x1804000
	s_nop 0
	v_addc_co_u32_e32 v7, vcc, 0, v181, vcc
	v_add_co_u32_e32 v8, vcc, s2, v180
	s_mov_b32 s2, 0x1808000
	s_nop 0
	v_addc_co_u32_e32 v9, vcc, 0, v181, vcc
	global_load_dwordx4 v[98:101], v[6:7], off sc0 nt
	global_load_dwordx4 v[106:109], v[8:9], off sc0 nt
	v_add_co_u32_e32 v6, vcc, s2, v180
	s_mov_b32 s2, 0x180c000
	s_nop 0
	v_addc_co_u32_e32 v7, vcc, 0, v181, vcc
	v_add_co_u32_e32 v8, vcc, s2, v180
	s_mov_b32 s2, 0x1810000
	s_nop 0
	v_addc_co_u32_e32 v9, vcc, 0, v181, vcc
	global_load_dwordx4 v[122:125], v[6:7], off sc0 nt
	global_load_dwordx4 v[82:85], v[8:9], off sc0 nt
	v_add_co_u32_e32 v6, vcc, s2, v180
	s_mov_b32 s2, 0x1814000
	s_nop 0
	v_addc_co_u32_e32 v7, vcc, 0, v181, vcc
	v_add_co_u32_e32 v8, vcc, s2, v180
	s_mov_b32 s2, 0x1818000
	s_nop 0
	v_addc_co_u32_e32 v9, vcc, 0, v181, vcc
	global_load_dwordx4 v[66:69], v[6:7], off sc0 nt
	global_load_dwordx4 v[74:77], v[8:9], off sc0 nt
	v_add_co_u32_e32 v6, vcc, s2, v180
	s_mov_b32 s2, 0x181c000
	s_nop 0
	v_addc_co_u32_e32 v7, vcc, 0, v181, vcc
	v_add_co_u32_e32 v8, vcc, s2, v180
	s_mov_b32 s2, 0x1820000
	s_nop 0
	v_addc_co_u32_e32 v9, vcc, 0, v181, vcc
	global_load_dwordx4 v[114:117], v[6:7], off sc0 nt
	global_load_dwordx4 v[58:61], v[8:9], off sc0 nt
	v_add_co_u32_e32 v6, vcc, s2, v180
	s_mov_b32 s2, 0x1824000
	s_nop 0
	v_addc_co_u32_e32 v7, vcc, 0, v181, vcc
	v_add_co_u32_e32 v8, vcc, s2, v180
	s_mov_b32 s2, 0x1828000
	s_nop 0
	v_addc_co_u32_e32 v9, vcc, 0, v181, vcc
	global_load_dwordx4 v[38:41], v[6:7], off sc0 nt
	global_load_dwordx4 v[46:49], v[8:9], off sc0 nt
	v_add_co_u32_e32 v6, vcc, s2, v180
	s_mov_b32 s2, 0x182c000
	s_nop 0
	v_addc_co_u32_e32 v7, vcc, 0, v181, vcc
	v_add_co_u32_e32 v8, vcc, s2, v180
	s_mov_b32 s2, 0x1830000
	s_nop 0
	v_addc_co_u32_e32 v9, vcc, 0, v181, vcc
	global_load_dwordx4 v[86:89], v[6:7], off sc0 nt
	global_load_dwordx4 v[30:33], v[8:9], off sc0 nt
	v_add_co_u32_e32 v6, vcc, s2, v180
	s_mov_b32 s2, 0x1834000
	s_nop 0
	v_addc_co_u32_e32 v7, vcc, 0, v181, vcc
	v_add_co_u32_e32 v8, vcc, s2, v180
	s_mov_b32 s2, 0x1838000
	s_nop 0
	v_addc_co_u32_e32 v9, vcc, 0, v181, vcc
	global_load_dwordx4 v[14:17], v[6:7], off sc0 nt
	global_load_dwordx4 v[22:25], v[8:9], off sc0 nt
	v_add_co_u32_e32 v6, vcc, s2, v180
	s_mov_b32 s2, 0x183c000
	s_nop 0
	v_addc_co_u32_e32 v7, vcc, 0, v181, vcc
	v_add_co_u32_e32 v8, vcc, s2, v180
	s_nop 1
	v_addc_co_u32_e32 v9, vcc, 0, v181, vcc
	global_load_dwordx4 v[62:65], v[6:7], off sc0 nt
	s_nop 0
	global_load_dwordx4 v[6:9], v[8:9], off sc0 nt
	ds_read_b128 v[130:133], v168
	ds_read_b128 v[134:137], v170
	ds_read_b128 v[138:141], v174
	ds_read_b128 v[142:145], v176
	s_waitcnt lgkmcnt(3)
	global_store_dwordx4 v[164:165], v[130:133], off offset:1024 nt
	s_waitcnt lgkmcnt(2)
	global_store_dwordx4 v[166:167], v[134:137], off offset:1024 nt
	s_waitcnt lgkmcnt(1)
	global_store_dwordx4 v[172:173], v[138:141], off offset:1024 nt
	s_waitcnt lgkmcnt(0)
	global_store_dwordx4 v[178:179], v[142:145], off offset:1024 nt
	s_waitcnt vmcnt(39)
	v_mul_f32_e32 v102, 0x43800000, v102
	s_waitcnt vmcnt(38)
	v_mul_f32_e32 v110, 0x43800000, v110
	v_med3_f32 v102, v102, s19, v1
	v_med3_f32 v110, v110, s19, v1
	v_mov_b32_e32 v130, v163
	v_cvt_pk_fp8_f32 v130, v102, v110
	s_waitcnt vmcnt(35)
	v_mul_f32_e32 v70, 0x43800000, v70
	s_waitcnt vmcnt(34)
	v_mul_f32_e32 v78, 0x43800000, v78
	v_med3_f32 v70, v70, s19, v1
	v_med3_f32 v78, v78, s19, v1
	v_mov_b32_e32 v131, v163
	v_mul_f32_e32 v126, 0x43800000, v126
	v_mul_f32_e32 v90, 0x43800000, v90
	v_cvt_pk_fp8_f32 v131, v70, v78
	s_waitcnt vmcnt(31)
	v_mul_f32_e32 v34, 0x43800000, v34
	s_waitcnt vmcnt(30)
	v_mul_f32_e32 v42, 0x43800000, v42
	v_med3_f32 v102, v126, s19, v1
	v_med3_f32 v90, v90, s19, v1
	v_med3_f32 v34, v34, s19, v1
	v_med3_f32 v42, v42, s19, v1
	v_mov_b32_e32 v132, v163
	v_cvt_pk_fp8_f32 v130, v102, v90 op_sel:[0,0,1]
	v_mul_f32_e32 v90, 0x43800000, v118
	v_mul_f32_e32 v50, 0x43800000, v50
	v_cvt_pk_fp8_f32 v132, v34, v42
	s_waitcnt vmcnt(27)
	v_mul_f32_e32 v10, 0x43800000, v10
	s_waitcnt vmcnt(26)
	v_mul_f32_e32 v18, 0x43800000, v18
	v_med3_f32 v70, v90, s19, v1
	v_med3_f32 v50, v50, s19, v1
	v_med3_f32 v10, v10, s19, v1
	v_med3_f32 v18, v18, s19, v1
	v_mov_b32_e32 v133, v163
	v_cvt_pk_fp8_f32 v131, v70, v50 op_sel:[0,0,1]
	v_mul_f32_e32 v50, 0x43800000, v94
	v_mul_f32_e32 v26, 0x43800000, v26
	v_cvt_pk_fp8_f32 v133, v10, v18
	v_med3_f32 v34, v50, s19, v1
	v_med3_f32 v26, v26, s19, v1
	v_cvt_pk_fp8_f32 v132, v34, v26 op_sel:[0,0,1]
	s_waitcnt vmcnt(25)
	v_mul_f32_e32 v26, 0x43800000, v54
	s_waitcnt vmcnt(24)
	v_mul_f32_e32 v2, 0x43800000, v2
	v_med3_f32 v10, v26, s19, v1
	v_med3_f32 v2, v2, s19, v1
	v_cvt_pk_fp8_f32 v133, v10, v2 op_sel:[0,0,1]
	v_mul_f32_e32 v2, 0x43800000, v103
	v_mul_f32_e32 v10, 0x43800000, v111
	v_med3_f32 v2, v2, s19, v1
	v_med3_f32 v10, v10, s19, v1
	v_mov_b32_e32 v134, v163
	v_cvt_pk_fp8_f32 v134, v2, v10
	v_mul_f32_e32 v18, 0x43800000, v127
	v_mul_f32_e32 v2, 0x43800000, v91
	v_med3_f32 v10, v18, s19, v1
	v_med3_f32 v2, v2, s19, v1
	v_cvt_pk_fp8_f32 v134, v10, v2 op_sel:[0,0,1]
	v_mul_f32_e32 v2, 0x43800000, v71
	v_mul_f32_e32 v10, 0x43800000, v79
	v_med3_f32 v2, v2, s19, v1
	v_med3_f32 v10, v10, s19, v1
	v_mov_b32_e32 v135, v163
	v_cvt_pk_fp8_f32 v135, v2, v10
	v_mul_f32_e32 v18, 0x43800000, v119
	v_mul_f32_e32 v2, 0x43800000, v51
	v_med3_f32 v10, v18, s19, v1
	v_med3_f32 v2, v2, s19, v1
	v_cvt_pk_fp8_f32 v135, v10, v2 op_sel:[0,0,1]
	v_mul_f32_e32 v2, 0x43800000, v35
	v_mul_f32_e32 v10, 0x43800000, v43
	v_med3_f32 v2, v2, s19, v1
	v_med3_f32 v10, v10, s19, v1
	v_mov_b32_e32 v136, v163
	v_cvt_pk_fp8_f32 v136, v2, v10
	v_mul_f32_e32 v18, 0x43800000, v95
	v_mul_f32_e32 v2, 0x43800000, v27
	v_med3_f32 v10, v18, s19, v1
	v_med3_f32 v2, v2, s19, v1
	v_cvt_pk_fp8_f32 v136, v10, v2 op_sel:[0,0,1]
	v_mul_f32_e32 v2, 0x43800000, v11
	v_mul_f32_e32 v10, 0x43800000, v19
	v_med3_f32 v2, v2, s19, v1
	v_med3_f32 v10, v10, s19, v1
	v_mov_b32_e32 v137, v163
	v_cvt_pk_fp8_f32 v137, v2, v10
	v_mul_f32_e32 v11, 0x43800000, v55
	v_mul_f32_e32 v2, 0x43800000, v3
	v_med3_f32 v3, v11, s19, v1
	v_med3_f32 v2, v2, s19, v1
	v_cvt_pk_fp8_f32 v137, v3, v2 op_sel:[0,0,1]
	v_mul_f32_e32 v2, 0x43800000, v104
	v_mul_f32_e32 v3, 0x43800000, v112
	v_med3_f32 v2, v2, s19, v1
	v_med3_f32 v3, v3, s19, v1
	v_mov_b32_e32 v138, v163
	v_cvt_pk_fp8_f32 v138, v2, v3
	v_mul_f32_e32 v10, 0x43800000, v128
	v_mul_f32_e32 v2, 0x43800000, v92
	v_med3_f32 v3, v10, s19, v1
	v_med3_f32 v2, v2, s19, v1
	v_cvt_pk_fp8_f32 v138, v3, v2 op_sel:[0,0,1]
	v_mul_f32_e32 v2, 0x43800000, v72
	v_mul_f32_e32 v3, 0x43800000, v80
	v_med3_f32 v2, v2, s19, v1
	v_med3_f32 v3, v3, s19, v1
	v_mov_b32_e32 v139, v163
	v_cvt_pk_fp8_f32 v139, v2, v3
	v_mul_f32_e32 v10, 0x43800000, v120
	v_mul_f32_e32 v2, 0x43800000, v52
	v_med3_f32 v3, v10, s19, v1
	v_med3_f32 v2, v2, s19, v1
	v_cvt_pk_fp8_f32 v139, v3, v2 op_sel:[0,0,1]
	v_mul_f32_e32 v2, 0x43800000, v36
	v_mul_f32_e32 v3, 0x43800000, v44
	v_med3_f32 v2, v2, s19, v1
	v_med3_f32 v3, v3, s19, v1
	v_mov_b32_e32 v140, v163
	v_cvt_pk_fp8_f32 v140, v2, v3
	v_mul_f32_e32 v10, 0x43800000, v96
	v_mul_f32_e32 v2, 0x43800000, v28
	v_med3_f32 v3, v10, s19, v1
	v_med3_f32 v2, v2, s19, v1
	v_cvt_pk_fp8_f32 v140, v3, v2 op_sel:[0,0,1]
	v_mul_f32_e32 v2, 0x43800000, v12
	v_mul_f32_e32 v3, 0x43800000, v20
	v_med3_f32 v2, v2, s19, v1
	v_med3_f32 v3, v3, s19, v1
	v_mov_b32_e32 v141, v163
	v_cvt_pk_fp8_f32 v141, v2, v3
	v_mul_f32_e32 v10, 0x43800000, v56
	v_mul_f32_e32 v2, 0x43800000, v4
	v_med3_f32 v3, v10, s19, v1
	v_med3_f32 v2, v2, s19, v1
	v_cvt_pk_fp8_f32 v141, v3, v2 op_sel:[0,0,1]
	v_mul_f32_e32 v2, 0x43800000, v105
	v_mul_f32_e32 v3, 0x43800000, v113
	v_med3_f32 v2, v2, s19, v1
	v_med3_f32 v3, v3, s19, v1
	v_mov_b32_e32 v10, v163
	v_cvt_pk_fp8_f32 v10, v2, v3
	v_mul_f32_e32 v4, 0x43800000, v129
	v_mul_f32_e32 v2, 0x43800000, v93
	v_med3_f32 v3, v4, s19, v1
	v_med3_f32 v2, v2, s19, v1
	v_cvt_pk_fp8_f32 v10, v3, v2 op_sel:[0,0,1]
	v_mul_f32_e32 v2, 0x43800000, v73
	v_mul_f32_e32 v3, 0x43800000, v81
	v_med3_f32 v2, v2, s19, v1
	v_med3_f32 v3, v3, s19, v1
	v_mov_b32_e32 v11, v163
	v_cvt_pk_fp8_f32 v11, v2, v3
	v_mul_f32_e32 v4, 0x43800000, v121
	v_mul_f32_e32 v2, 0x43800000, v53
	v_med3_f32 v3, v4, s19, v1
	v_med3_f32 v2, v2, s19, v1
	v_cvt_pk_fp8_f32 v11, v3, v2 op_sel:[0,0,1]
	v_mul_f32_e32 v2, 0x43800000, v37
	v_mul_f32_e32 v3, 0x43800000, v45
	v_med3_f32 v2, v2, s19, v1
	v_med3_f32 v3, v3, s19, v1
	v_mov_b32_e32 v12, v163
	v_cvt_pk_fp8_f32 v12, v2, v3
	v_mul_f32_e32 v4, 0x43800000, v97
	v_mul_f32_e32 v2, 0x43800000, v29
	v_med3_f32 v3, v4, s19, v1
	v_med3_f32 v2, v2, s19, v1
	v_cvt_pk_fp8_f32 v12, v3, v2 op_sel:[0,0,1]
	v_mul_f32_e32 v2, 0x43800000, v13
	v_mul_f32_e32 v3, 0x43800000, v21
	v_med3_f32 v2, v2, s19, v1
	v_med3_f32 v3, v3, s19, v1
	v_mov_b32_e32 v13, v163
	v_cvt_pk_fp8_f32 v13, v2, v3
	v_mul_f32_e32 v4, 0x43800000, v57
	v_mul_f32_e32 v2, 0x43800000, v5
	v_med3_f32 v3, v4, s19, v1
	v_med3_f32 v2, v2, s19, v1
	v_cvt_pk_fp8_f32 v13, v3, v2 op_sel:[0,0,1]
	ds_write_b128 v182, v[130:133] offset:34816
	ds_write_b128 v182, v[134:137] offset:35088
	ds_write_b128 v182, v[138:141] offset:35360
	ds_write_b128 v182, v[10:13] offset:35632
	s_waitcnt lgkmcnt(0)
	s_barrier
	s_mov_b32 s2, 0x1c00000
	v_add_co_u32_e32 v2, vcc, s2, v180
	s_mov_b32 s2, 0x1c04000
	s_nop 0
	v_addc_co_u32_e32 v3, vcc, 0, v181, vcc
	v_add_co_u32_e32 v4, vcc, s2, v180
	s_mov_b32 s2, 0x1c08000
	s_nop 0
	v_addc_co_u32_e32 v5, vcc, 0, v181, vcc
	global_load_dwordx4 v[102:105], v[2:3], off sc0 nt
	global_load_dwordx4 v[110:113], v[4:5], off sc0 nt
	v_add_co_u32_e32 v2, vcc, s2, v180
	s_mov_b32 s2, 0x1c0c000
	s_nop 0
	v_addc_co_u32_e32 v3, vcc, 0, v181, vcc
	v_add_co_u32_e32 v4, vcc, s2, v180
	s_mov_b32 s2, 0x1c10000
	s_nop 0
	v_addc_co_u32_e32 v5, vcc, 0, v181, vcc
	global_load_dwordx4 v[126:129], v[2:3], off sc0 nt
	global_load_dwordx4 v[90:93], v[4:5], off sc0 nt
	v_add_co_u32_e32 v2, vcc, s2, v180
	s_mov_b32 s2, 0x1c14000
	s_nop 0
	v_addc_co_u32_e32 v3, vcc, 0, v181, vcc
	v_add_co_u32_e32 v4, vcc, s2, v180
	s_mov_b32 s2, 0x1c18000
	s_nop 0
	v_addc_co_u32_e32 v5, vcc, 0, v181, vcc
	global_load_dwordx4 v[70:73], v[2:3], off sc0 nt
	global_load_dwordx4 v[78:81], v[4:5], off sc0 nt
	v_add_co_u32_e32 v2, vcc, s2, v180
	s_mov_b32 s2, 0x1c1c000
	s_nop 0
	v_addc_co_u32_e32 v3, vcc, 0, v181, vcc
	v_add_co_u32_e32 v4, vcc, s2, v180
	s_mov_b32 s2, 0x1c20000
	s_nop 0
	v_addc_co_u32_e32 v5, vcc, 0, v181, vcc
	global_load_dwordx4 v[118:121], v[2:3], off sc0 nt
	global_load_dwordx4 v[50:53], v[4:5], off sc0 nt
	v_add_co_u32_e32 v2, vcc, s2, v180
	s_mov_b32 s2, 0x1c24000
	s_nop 0
	v_addc_co_u32_e32 v3, vcc, 0, v181, vcc
	v_add_co_u32_e32 v4, vcc, s2, v180
	s_mov_b32 s2, 0x1c28000
	s_nop 0
	v_addc_co_u32_e32 v5, vcc, 0, v181, vcc
	global_load_dwordx4 v[34:37], v[2:3], off sc0 nt
	global_load_dwordx4 v[42:45], v[4:5], off sc0 nt
	v_add_co_u32_e32 v2, vcc, s2, v180
	s_mov_b32 s2, 0x1c2c000
	s_nop 0
	v_addc_co_u32_e32 v3, vcc, 0, v181, vcc
	v_add_co_u32_e32 v4, vcc, s2, v180
	s_mov_b32 s2, 0x1c30000
	s_nop 0
	v_addc_co_u32_e32 v5, vcc, 0, v181, vcc
	global_load_dwordx4 v[94:97], v[2:3], off sc0 nt
	global_load_dwordx4 v[26:29], v[4:5], off sc0 nt
	v_add_co_u32_e32 v2, vcc, s2, v180
	s_mov_b32 s2, 0x1c34000
	s_nop 0
	v_addc_co_u32_e32 v3, vcc, 0, v181, vcc
	v_add_co_u32_e32 v4, vcc, s2, v180
	s_mov_b32 s2, 0x1c38000
	s_nop 0
	v_addc_co_u32_e32 v5, vcc, 0, v181, vcc
	global_load_dwordx4 v[10:13], v[2:3], off sc0 nt
	global_load_dwordx4 v[18:21], v[4:5], off sc0 nt
	v_add_co_u32_e32 v2, vcc, s2, v180
	s_mov_b32 s2, 0x1c3c000
	s_nop 0
	v_addc_co_u32_e32 v3, vcc, 0, v181, vcc
	v_add_co_u32_e32 v4, vcc, s2, v180
	s_nop 1
	v_addc_co_u32_e32 v5, vcc, 0, v181, vcc
	global_load_dwordx4 v[54:57], v[2:3], off sc0 nt
	s_nop 0
	global_load_dwordx4 v[2:5], v[4:5], off sc0 nt
	ds_read_b128 v[130:133], v168 offset:34816
	ds_read_b128 v[134:137], v170 offset:34816
	ds_read_b128 v[138:141], v174 offset:34816
	ds_read_b128 v[142:145], v176 offset:34816
	s_waitcnt lgkmcnt(3)
	global_store_dwordx4 v[164:165], v[130:133], off offset:1280 nt
	s_waitcnt lgkmcnt(2)
	global_store_dwordx4 v[166:167], v[134:137], off offset:1280 nt
	s_waitcnt lgkmcnt(1)
	global_store_dwordx4 v[172:173], v[138:141], off offset:1280 nt
	s_waitcnt lgkmcnt(0)
	global_store_dwordx4 v[178:179], v[142:145], off offset:1280 nt
	s_waitcnt vmcnt(39)
	v_mul_f32_e32 v98, 0x43800000, v98
	s_waitcnt vmcnt(38)
	v_mul_f32_e32 v106, 0x43800000, v106
	v_med3_f32 v98, v98, s19, v1
	v_med3_f32 v106, v106, s19, v1
	v_mov_b32_e32 v130, v163
	v_cvt_pk_fp8_f32 v130, v98, v106
	s_waitcnt vmcnt(35)
	v_mul_f32_e32 v66, 0x43800000, v66
	s_waitcnt vmcnt(34)
	v_mul_f32_e32 v74, 0x43800000, v74
	v_med3_f32 v66, v66, s19, v1
	v_med3_f32 v74, v74, s19, v1
	v_mov_b32_e32 v131, v163
	v_mul_f32_e32 v122, 0x43800000, v122
	v_mul_f32_e32 v82, 0x43800000, v82
	v_cvt_pk_fp8_f32 v131, v66, v74
	s_waitcnt vmcnt(31)
	v_mul_f32_e32 v38, 0x43800000, v38
	s_waitcnt vmcnt(30)
	v_mul_f32_e32 v46, 0x43800000, v46
	v_med3_f32 v98, v122, s19, v1
	v_med3_f32 v82, v82, s19, v1
	v_med3_f32 v38, v38, s19, v1
	v_med3_f32 v46, v46, s19, v1
	v_mov_b32_e32 v132, v163
	v_cvt_pk_fp8_f32 v130, v98, v82 op_sel:[0,0,1]
	v_mul_f32_e32 v82, 0x43800000, v114
	v_mul_f32_e32 v58, 0x43800000, v58
	v_cvt_pk_fp8_f32 v132, v38, v46
	s_waitcnt vmcnt(27)
	v_mul_f32_e32 v14, 0x43800000, v14
	s_waitcnt vmcnt(26)
	v_mul_f32_e32 v22, 0x43800000, v22
	v_med3_f32 v66, v82, s19, v1
	v_med3_f32 v58, v58, s19, v1
	v_med3_f32 v14, v14, s19, v1
	v_med3_f32 v22, v22, s19, v1
	v_mov_b32_e32 v133, v163
	v_cvt_pk_fp8_f32 v131, v66, v58 op_sel:[0,0,1]
	v_mul_f32_e32 v58, 0x43800000, v86
	v_mul_f32_e32 v30, 0x43800000, v30
	v_cvt_pk_fp8_f32 v133, v14, v22
	v_med3_f32 v38, v58, s19, v1
	v_med3_f32 v30, v30, s19, v1
	v_cvt_pk_fp8_f32 v132, v38, v30 op_sel:[0,0,1]
	s_waitcnt vmcnt(25)
	v_mul_f32_e32 v30, 0x43800000, v62
	s_waitcnt vmcnt(24)
	v_mul_f32_e32 v6, 0x43800000, v6
	v_med3_f32 v14, v30, s19, v1
	v_med3_f32 v6, v6, s19, v1
	v_cvt_pk_fp8_f32 v133, v14, v6 op_sel:[0,0,1]
	v_mul_f32_e32 v6, 0x43800000, v99
	v_mul_f32_e32 v14, 0x43800000, v107
	v_med3_f32 v6, v6, s19, v1
	v_med3_f32 v14, v14, s19, v1
	v_mov_b32_e32 v134, v163
	v_cvt_pk_fp8_f32 v134, v6, v14
	v_mul_f32_e32 v22, 0x43800000, v123
	v_mul_f32_e32 v6, 0x43800000, v83
	v_med3_f32 v14, v22, s19, v1
	v_med3_f32 v6, v6, s19, v1
	v_cvt_pk_fp8_f32 v134, v14, v6 op_sel:[0,0,1]
	v_mul_f32_e32 v6, 0x43800000, v67
	v_mul_f32_e32 v14, 0x43800000, v75
	v_med3_f32 v6, v6, s19, v1
	v_med3_f32 v14, v14, s19, v1
	v_mov_b32_e32 v135, v163
	v_cvt_pk_fp8_f32 v135, v6, v14
	v_mul_f32_e32 v22, 0x43800000, v115
	v_mul_f32_e32 v6, 0x43800000, v59
	v_med3_f32 v14, v22, s19, v1
	v_med3_f32 v6, v6, s19, v1
	v_cvt_pk_fp8_f32 v135, v14, v6 op_sel:[0,0,1]
	v_mul_f32_e32 v6, 0x43800000, v39
	v_mul_f32_e32 v14, 0x43800000, v47
	v_med3_f32 v6, v6, s19, v1
	v_med3_f32 v14, v14, s19, v1
	v_mov_b32_e32 v136, v163
	v_cvt_pk_fp8_f32 v136, v6, v14
	v_mul_f32_e32 v22, 0x43800000, v87
	v_mul_f32_e32 v6, 0x43800000, v31
	v_med3_f32 v14, v22, s19, v1
	v_med3_f32 v6, v6, s19, v1
	v_cvt_pk_fp8_f32 v136, v14, v6 op_sel:[0,0,1]
	v_mul_f32_e32 v6, 0x43800000, v15
	v_mul_f32_e32 v14, 0x43800000, v23
	v_med3_f32 v6, v6, s19, v1
	v_med3_f32 v14, v14, s19, v1
	v_mov_b32_e32 v137, v163
	v_cvt_pk_fp8_f32 v137, v6, v14
	v_mul_f32_e32 v15, 0x43800000, v63
	v_mul_f32_e32 v6, 0x43800000, v7
	v_med3_f32 v7, v15, s19, v1
	v_med3_f32 v6, v6, s19, v1
	v_cvt_pk_fp8_f32 v137, v7, v6 op_sel:[0,0,1]
	v_mul_f32_e32 v6, 0x43800000, v100
	v_mul_f32_e32 v7, 0x43800000, v108
	v_med3_f32 v6, v6, s19, v1
	v_med3_f32 v7, v7, s19, v1
	v_mov_b32_e32 v138, v163
	v_cvt_pk_fp8_f32 v138, v6, v7
	v_mul_f32_e32 v14, 0x43800000, v124
	v_mul_f32_e32 v6, 0x43800000, v84
	v_med3_f32 v7, v14, s19, v1
	v_med3_f32 v6, v6, s19, v1
	v_cvt_pk_fp8_f32 v138, v7, v6 op_sel:[0,0,1]
	v_mul_f32_e32 v6, 0x43800000, v68
	v_mul_f32_e32 v7, 0x43800000, v76
	v_med3_f32 v6, v6, s19, v1
	v_med3_f32 v7, v7, s19, v1
	v_mov_b32_e32 v139, v163
	v_cvt_pk_fp8_f32 v139, v6, v7
	v_mul_f32_e32 v14, 0x43800000, v116
	v_mul_f32_e32 v6, 0x43800000, v60
	v_med3_f32 v7, v14, s19, v1
	v_med3_f32 v6, v6, s19, v1
	v_cvt_pk_fp8_f32 v139, v7, v6 op_sel:[0,0,1]
	v_mul_f32_e32 v6, 0x43800000, v40
	v_mul_f32_e32 v7, 0x43800000, v48
	v_med3_f32 v6, v6, s19, v1
	v_med3_f32 v7, v7, s19, v1
	v_mov_b32_e32 v140, v163
	v_cvt_pk_fp8_f32 v140, v6, v7
	v_mul_f32_e32 v14, 0x43800000, v88
	v_mul_f32_e32 v6, 0x43800000, v32
	v_med3_f32 v7, v14, s19, v1
	v_med3_f32 v6, v6, s19, v1
	v_cvt_pk_fp8_f32 v140, v7, v6 op_sel:[0,0,1]
	v_mul_f32_e32 v6, 0x43800000, v16
	v_mul_f32_e32 v7, 0x43800000, v24
	v_med3_f32 v6, v6, s19, v1
	v_med3_f32 v7, v7, s19, v1
	v_mov_b32_e32 v141, v163
	v_cvt_pk_fp8_f32 v141, v6, v7
	v_mul_f32_e32 v14, 0x43800000, v64
	v_mul_f32_e32 v6, 0x43800000, v8
	v_med3_f32 v7, v14, s19, v1
	v_med3_f32 v6, v6, s19, v1
	v_cvt_pk_fp8_f32 v141, v7, v6 op_sel:[0,0,1]
	v_mul_f32_e32 v6, 0x43800000, v101
	v_mul_f32_e32 v7, 0x43800000, v109
	v_med3_f32 v6, v6, s19, v1
	v_med3_f32 v7, v7, s19, v1
	v_mov_b32_e32 v14, v163
	v_cvt_pk_fp8_f32 v14, v6, v7
	v_mul_f32_e32 v8, 0x43800000, v125
	v_mul_f32_e32 v6, 0x43800000, v85
	v_med3_f32 v7, v8, s19, v1
	v_med3_f32 v6, v6, s19, v1
	v_cvt_pk_fp8_f32 v14, v7, v6 op_sel:[0,0,1]
	v_mul_f32_e32 v6, 0x43800000, v69
	v_mul_f32_e32 v7, 0x43800000, v77
	v_med3_f32 v6, v6, s19, v1
	v_med3_f32 v7, v7, s19, v1
	v_mov_b32_e32 v15, v163
	v_cvt_pk_fp8_f32 v15, v6, v7
	v_mul_f32_e32 v8, 0x43800000, v117
	v_mul_f32_e32 v6, 0x43800000, v61
	v_med3_f32 v7, v8, s19, v1
	v_med3_f32 v6, v6, s19, v1
	v_cvt_pk_fp8_f32 v15, v7, v6 op_sel:[0,0,1]
	v_mul_f32_e32 v6, 0x43800000, v41
	v_mul_f32_e32 v7, 0x43800000, v49
	v_med3_f32 v6, v6, s19, v1
	v_med3_f32 v7, v7, s19, v1
	v_mov_b32_e32 v16, v163
	v_cvt_pk_fp8_f32 v16, v6, v7
	v_mul_f32_e32 v8, 0x43800000, v89
	v_mul_f32_e32 v6, 0x43800000, v33
	v_med3_f32 v7, v8, s19, v1
	v_med3_f32 v6, v6, s19, v1
	v_cvt_pk_fp8_f32 v16, v7, v6 op_sel:[0,0,1]
	v_mul_f32_e32 v6, 0x43800000, v17
	v_mul_f32_e32 v7, 0x43800000, v25
	v_med3_f32 v6, v6, s19, v1
	v_med3_f32 v7, v7, s19, v1
	v_mov_b32_e32 v17, v163
	v_cvt_pk_fp8_f32 v17, v6, v7
	v_mul_f32_e32 v8, 0x43800000, v65
	v_mul_f32_e32 v6, 0x43800000, v9
	v_med3_f32 v7, v8, s19, v1
	v_med3_f32 v6, v6, s19, v1
	v_cvt_pk_fp8_f32 v17, v7, v6 op_sel:[0,0,1]
	ds_write_b128 v182, v[130:133]
	ds_write_b128 v182, v[134:137] offset:272
	ds_write_b128 v182, v[138:141] offset:544
	ds_write_b128 v182, v[14:17] offset:816
	s_waitcnt lgkmcnt(0)
	s_barrier
	ds_read_b128 v[6:9], v168
	ds_read_b128 v[14:17], v170
	ds_read_b128 v[22:25], v174
	ds_read_b128 v[30:33], v176
	s_waitcnt lgkmcnt(3)
	global_store_dwordx4 v[164:165], v[6:9], off offset:1536 nt
	s_waitcnt lgkmcnt(2)
	global_store_dwordx4 v[166:167], v[14:17], off offset:1536 nt
	s_waitcnt lgkmcnt(1)
	global_store_dwordx4 v[172:173], v[22:25], off offset:1536 nt
	s_waitcnt lgkmcnt(0)
	global_store_dwordx4 v[178:179], v[30:33], off offset:1536 nt
	s_waitcnt vmcnt(23)
	v_mul_f32_e32 v6, 0x43800000, v102
	s_waitcnt vmcnt(22)
	v_mul_f32_e32 v7, 0x43800000, v110
	v_med3_f32 v9, v6, s19, v1
	v_med3_f32 v7, v7, s19, v1
	v_mov_b32_e32 v6, v163
	v_cvt_pk_fp8_f32 v6, v9, v7
	s_waitcnt vmcnt(21)
	v_mul_f32_e32 v8, 0x43800000, v126
	s_waitcnt vmcnt(20)
	v_mul_f32_e32 v7, 0x43800000, v90
	v_med3_f32 v8, v8, s19, v1
	v_med3_f32 v7, v7, s19, v1
	v_cvt_pk_fp8_f32 v6, v8, v7 op_sel:[0,0,1]
	s_waitcnt vmcnt(19)
	v_mul_f32_e32 v7, 0x43800000, v70
	s_waitcnt vmcnt(18)
	v_mul_f32_e32 v8, 0x43800000, v78
	v_med3_f32 v14, v7, s19, v1
	v_med3_f32 v8, v8, s19, v1
	v_mov_b32_e32 v7, v163
	v_cvt_pk_fp8_f32 v7, v14, v8
	s_waitcnt vmcnt(17)
	v_mul_f32_e32 v9, 0x43800000, v118
	s_waitcnt vmcnt(16)
	v_mul_f32_e32 v8, 0x43800000, v50
	v_med3_f32 v9, v9, s19, v1
	v_med3_f32 v8, v8, s19, v1
	v_cvt_pk_fp8_f32 v7, v9, v8 op_sel:[0,0,1]
	s_waitcnt vmcnt(15)
	v_mul_f32_e32 v8, 0x43800000, v34
	s_waitcnt vmcnt(14)
	v_mul_f32_e32 v9, 0x43800000, v42
	v_med3_f32 v15, v8, s19, v1
	v_med3_f32 v9, v9, s19, v1
	v_mov_b32_e32 v8, v163
	v_cvt_pk_fp8_f32 v8, v15, v9
	s_waitcnt vmcnt(13)
	v_mul_f32_e32 v14, 0x43800000, v94
	s_waitcnt vmcnt(12)
	v_mul_f32_e32 v9, 0x43800000, v26
	v_med3_f32 v14, v14, s19, v1
	v_med3_f32 v9, v9, s19, v1
	v_cvt_pk_fp8_f32 v8, v14, v9 op_sel:[0,0,1]
	s_waitcnt vmcnt(11)
	v_mul_f32_e32 v9, 0x43800000, v10
	s_waitcnt vmcnt(10)
	v_mul_f32_e32 v10, 0x43800000, v18
	v_med3_f32 v15, v9, s19, v1
	v_med3_f32 v10, v10, s19, v1
	v_mov_b32_e32 v9, v163
	v_cvt_pk_fp8_f32 v9, v15, v10
	s_waitcnt vmcnt(9)
	v_mul_f32_e32 v14, 0x43800000, v54
	s_waitcnt vmcnt(8)
	v_mul_f32_e32 v2, 0x43800000, v2
	v_med3_f32 v10, v14, s19, v1
	v_med3_f32 v2, v2, s19, v1
	v_cvt_pk_fp8_f32 v9, v10, v2 op_sel:[0,0,1]
	v_mul_f32_e32 v2, 0x43800000, v103
	v_mul_f32_e32 v10, 0x43800000, v111
	v_med3_f32 v2, v2, s19, v1
	v_med3_f32 v10, v10, s19, v1
	v_mov_b32_e32 v14, v163
	v_cvt_pk_fp8_f32 v14, v2, v10
	v_mul_f32_e32 v15, 0x43800000, v127
	v_mul_f32_e32 v2, 0x43800000, v91
	v_med3_f32 v10, v15, s19, v1
	v_med3_f32 v2, v2, s19, v1
	v_cvt_pk_fp8_f32 v14, v10, v2 op_sel:[0,0,1]
	v_mul_f32_e32 v2, 0x43800000, v71
	v_mul_f32_e32 v10, 0x43800000, v79
	v_med3_f32 v2, v2, s19, v1
	v_med3_f32 v10, v10, s19, v1
	v_mov_b32_e32 v15, v163
	v_cvt_pk_fp8_f32 v15, v2, v10
	v_mul_f32_e32 v16, 0x43800000, v119
	v_mul_f32_e32 v2, 0x43800000, v51
	v_med3_f32 v10, v16, s19, v1
	v_med3_f32 v2, v2, s19, v1
	v_cvt_pk_fp8_f32 v15, v10, v2 op_sel:[0,0,1]
	v_mul_f32_e32 v2, 0x43800000, v35
	v_mul_f32_e32 v10, 0x43800000, v43
	v_med3_f32 v2, v2, s19, v1
	v_med3_f32 v10, v10, s19, v1
	v_mov_b32_e32 v16, v163
	v_cvt_pk_fp8_f32 v16, v2, v10
	v_mul_f32_e32 v17, 0x43800000, v95
	v_mul_f32_e32 v2, 0x43800000, v27
	v_med3_f32 v10, v17, s19, v1
	v_med3_f32 v2, v2, s19, v1
	v_cvt_pk_fp8_f32 v16, v10, v2 op_sel:[0,0,1]
	v_mul_f32_e32 v2, 0x43800000, v11
	v_mul_f32_e32 v10, 0x43800000, v19
	v_med3_f32 v2, v2, s19, v1
	v_med3_f32 v10, v10, s19, v1
	v_mov_b32_e32 v17, v163
	v_cvt_pk_fp8_f32 v17, v2, v10
	v_mul_f32_e32 v11, 0x43800000, v55
	v_mul_f32_e32 v2, 0x43800000, v3
	v_med3_f32 v3, v11, s19, v1
	v_med3_f32 v2, v2, s19, v1
	v_cvt_pk_fp8_f32 v17, v3, v2 op_sel:[0,0,1]
	v_mul_f32_e32 v2, 0x43800000, v104
	v_mul_f32_e32 v3, 0x43800000, v112
	v_med3_f32 v2, v2, s19, v1
	v_med3_f32 v3, v3, s19, v1
	v_mov_b32_e32 v22, v163
	v_cvt_pk_fp8_f32 v22, v2, v3
	v_mul_f32_e32 v10, 0x43800000, v128
	v_mul_f32_e32 v2, 0x43800000, v92
	v_med3_f32 v3, v10, s19, v1
	v_med3_f32 v2, v2, s19, v1
	v_cvt_pk_fp8_f32 v22, v3, v2 op_sel:[0,0,1]
	v_mul_f32_e32 v2, 0x43800000, v72
	v_mul_f32_e32 v3, 0x43800000, v80
	v_med3_f32 v2, v2, s19, v1
	v_med3_f32 v3, v3, s19, v1
	v_mov_b32_e32 v23, v163
	v_cvt_pk_fp8_f32 v23, v2, v3
	v_mul_f32_e32 v10, 0x43800000, v120
	v_mul_f32_e32 v2, 0x43800000, v52
	v_med3_f32 v3, v10, s19, v1
	v_med3_f32 v2, v2, s19, v1
	v_cvt_pk_fp8_f32 v23, v3, v2 op_sel:[0,0,1]
	v_mul_f32_e32 v2, 0x43800000, v36
	v_mul_f32_e32 v3, 0x43800000, v44
	v_med3_f32 v2, v2, s19, v1
	v_med3_f32 v3, v3, s19, v1
	v_mov_b32_e32 v24, v163
	v_cvt_pk_fp8_f32 v24, v2, v3
	v_mul_f32_e32 v10, 0x43800000, v96
	v_mul_f32_e32 v2, 0x43800000, v28
	v_med3_f32 v3, v10, s19, v1
	v_med3_f32 v2, v2, s19, v1
	v_cvt_pk_fp8_f32 v24, v3, v2 op_sel:[0,0,1]
	v_mul_f32_e32 v2, 0x43800000, v12
	v_mul_f32_e32 v3, 0x43800000, v20
	v_med3_f32 v2, v2, s19, v1
	v_med3_f32 v3, v3, s19, v1
	v_mov_b32_e32 v25, v163
	v_cvt_pk_fp8_f32 v25, v2, v3
	v_mul_f32_e32 v10, 0x43800000, v56
	v_mul_f32_e32 v2, 0x43800000, v4
	v_med3_f32 v3, v10, s19, v1
	v_med3_f32 v2, v2, s19, v1
	v_cvt_pk_fp8_f32 v25, v3, v2 op_sel:[0,0,1]
	v_mul_f32_e32 v2, 0x43800000, v105
	v_mul_f32_e32 v3, 0x43800000, v113
	v_med3_f32 v2, v2, s19, v1
	v_med3_f32 v3, v3, s19, v1
	v_mov_b32_e32 v10, v163
	v_cvt_pk_fp8_f32 v10, v2, v3
	v_mul_f32_e32 v4, 0x43800000, v129
	v_mul_f32_e32 v2, 0x43800000, v93
	v_med3_f32 v3, v4, s19, v1
	v_med3_f32 v2, v2, s19, v1
	v_cvt_pk_fp8_f32 v10, v3, v2 op_sel:[0,0,1]
	v_mul_f32_e32 v2, 0x43800000, v73
	v_mul_f32_e32 v3, 0x43800000, v81
	v_med3_f32 v2, v2, s19, v1
	v_med3_f32 v3, v3, s19, v1
	v_mov_b32_e32 v11, v163
	v_cvt_pk_fp8_f32 v11, v2, v3
	v_mul_f32_e32 v4, 0x43800000, v121
	v_mul_f32_e32 v2, 0x43800000, v53
	v_med3_f32 v3, v4, s19, v1
	v_med3_f32 v2, v2, s19, v1
	v_cvt_pk_fp8_f32 v11, v3, v2 op_sel:[0,0,1]
	v_mul_f32_e32 v2, 0x43800000, v37
	v_mul_f32_e32 v3, 0x43800000, v45
	v_med3_f32 v2, v2, s19, v1
	v_med3_f32 v3, v3, s19, v1
	v_mov_b32_e32 v12, v163
	v_cvt_pk_fp8_f32 v12, v2, v3
	v_mul_f32_e32 v4, 0x43800000, v97
	v_mul_f32_e32 v2, 0x43800000, v29
	v_med3_f32 v3, v4, s19, v1
	v_med3_f32 v2, v2, s19, v1
	v_cvt_pk_fp8_f32 v12, v3, v2 op_sel:[0,0,1]
	v_mul_f32_e32 v2, 0x43800000, v13
	v_mul_f32_e32 v3, 0x43800000, v21
	v_med3_f32 v2, v2, s19, v1
	v_med3_f32 v3, v3, s19, v1
	v_mov_b32_e32 v13, v163
	v_cvt_pk_fp8_f32 v13, v2, v3
	v_mul_f32_e32 v4, 0x43800000, v57
	v_mul_f32_e32 v2, 0x43800000, v5
	v_med3_f32 v3, v4, s19, v1
	v_med3_f32 v2, v2, s19, v1
	v_cvt_pk_fp8_f32 v13, v3, v2 op_sel:[0,0,1]
	ds_write_b128 v182, v[6:9] offset:34816
	ds_write_b128 v182, v[14:17] offset:35088
	ds_write_b128 v182, v[22:25] offset:35360
	ds_write_b128 v182, v[10:13] offset:35632
	s_waitcnt lgkmcnt(0)
	s_barrier
	ds_read_b128 v[2:5], v168 offset:34816
	ds_read_b128 v[6:9], v170 offset:34816
	ds_read_b128 v[10:13], v174 offset:34816
	ds_read_b128 v[14:17], v176 offset:34816
	s_waitcnt lgkmcnt(3)
	global_store_dwordx4 v[164:165], v[2:5], off offset:1792 nt
	s_waitcnt lgkmcnt(2)
	global_store_dwordx4 v[166:167], v[6:9], off offset:1792 nt
	s_waitcnt lgkmcnt(1)
	global_store_dwordx4 v[172:173], v[10:13], off offset:1792 nt
	s_waitcnt lgkmcnt(0)
	global_store_dwordx4 v[178:179], v[14:17], off offset:1792 nt
	s_barrier
	s_branch .LBB0_162

.LBB0_168:
	s_cmpk_gt_i32 s4, 0x3ff
	s_mov_b64 s[30:31], -1
	s_cbranch_scc0 .LBB0_170
	s_add_i32 s0, s4, 0xfffffc00
	s_lshr_b32 s12, s0, 4
	v_readlane_b32 s56, v254, 4
	s_lshl_b64 s[0:1], s[12:13], 24
	v_readlane_b32 s62, v254, 10
	v_readlane_b32 s63, v254, 11
	s_add_u32 s0, s62, s0
	s_addc_u32 s1, s63, s1
	s_lshl_b32 s6, s4, 7
	s_and_b32 s11, s6, 0x780
	s_lshl_b32 s6, s11, 2
	s_add_u32 s6, s0, s6
	s_addc_u32 s7, s1, 0
	s_lshl_b64 s[0:1], s[12:13], 22
	s_lshl_b32 s11, s11, 11
	v_readlane_b32 s2, v255, 1
	s_add_u32 s0, s2, s0
	v_readlane_b32 s2, v255, 3
	v_mov_b32_e32 v130, v0
	s_addc_u32 s1, s2, s1
	s_add_u32 s30, s0, s11
	v_readfirstlane_b32 s10, v130
	s_addc_u32 s31, s1, 0
	s_ashr_i32 s0, s10, 1
	v_lshrrev_b32_e32 v2, 1, v130
	s_andn2_b32 s0, s0, 31
	v_and_b32_e32 v131, 16, v2
	v_or_b32_e32 v2, s0, v131
	v_ashrrev_i32_e32 v3, 31, v2
	s_waitcnt lgkmcnt(0)
	v_lshlrev_b32_e32 v4, 2, v130
	v_lshlrev_b64 v[2:3], 13, v[2:3]
	v_and_b32_e32 v136, 0x7c, v4
	v_lshl_add_u64 v[2:3], s[6:7], 0, v[2:3]
	v_lshlrev_b32_e32 v154, 2, v136
	v_lshl_add_u64 v[162:163], v[2:3], 0, v[154:155]
	s_movk_i32 s1, 0x2000
	v_add_co_u32_e32 v2, vcc, s1, v162
	s_movk_i32 s1, 0x6000
	s_nop 0
	v_addc_co_u32_e32 v3, vcc, 0, v163, vcc
	global_load_dwordx4 v[86:89], v[162:163], off sc0 nt
	global_load_dwordx4 v[94:97], v[2:3], off sc0 nt
	v_add_co_u32_e32 v2, vcc, s35, v162
	v_readlane_b32 s57, v254, 5
	s_nop 0
	v_addc_co_u32_e32 v3, vcc, 0, v163, vcc
	v_add_co_u32_e32 v4, vcc, s1, v162
	s_mov_b32 s1, 0xa000
	s_nop 0
	v_addc_co_u32_e32 v5, vcc, 0, v163, vcc
	global_load_dwordx4 v[114:117], v[2:3], off sc0 nt
	global_load_dwordx4 v[118:121], v[4:5], off sc0 nt
	v_add_co_u32_e32 v2, vcc, s36, v162
	v_readlane_b32 s58, v254, 6
	s_nop 0
	v_addc_co_u32_e32 v3, vcc, 0, v163, vcc
	v_add_co_u32_e32 v4, vcc, s1, v162
	s_mov_b32 s1, 0xe000
	s_nop 0
	v_addc_co_u32_e32 v5, vcc, 0, v163, vcc
	global_load_dwordx4 v[54:57], v[2:3], off sc0 nt
	global_load_dwordx4 v[62:65], v[4:5], off sc0 nt
	v_add_co_u32_e32 v2, vcc, s37, v162
	v_readlane_b32 s59, v254, 7
	s_nop 0
	v_addc_co_u32_e32 v3, vcc, 0, v163, vcc
	v_add_co_u32_e32 v4, vcc, s1, v162
	s_mov_b32 s1, 0x12000
	s_nop 0
	v_addc_co_u32_e32 v5, vcc, 0, v163, vcc
	global_load_dwordx4 v[82:85], v[2:3], off sc0 nt
	global_load_dwordx4 v[90:93], v[4:5], off sc0 nt
	v_add_co_u32_e32 v2, vcc, s38, v162
	v_readlane_b32 s60, v254, 8
	s_nop 0
	v_addc_co_u32_e32 v3, vcc, 0, v163, vcc
	v_add_co_u32_e32 v4, vcc, s1, v162
	s_mov_b32 s1, 0x16000
	s_nop 0
	v_addc_co_u32_e32 v5, vcc, 0, v163, vcc
	global_load_dwordx4 v[22:25], v[2:3], off sc0 nt
	global_load_dwordx4 v[30:33], v[4:5], off sc0 nt
	v_add_co_u32_e32 v2, vcc, s39, v162
	v_readlane_b32 s61, v254, 9
	s_nop 0
	v_addc_co_u32_e32 v3, vcc, 0, v163, vcc
	v_add_co_u32_e32 v4, vcc, s1, v162
	s_mov_b32 s1, 0x1a000
	s_nop 0
	v_addc_co_u32_e32 v5, vcc, 0, v163, vcc
	global_load_dwordx4 v[46:49], v[2:3], off sc0 nt
	global_load_dwordx4 v[58:61], v[4:5], off sc0 nt
	v_add_co_u32_e32 v2, vcc, s40, v162
	s_nop 1
	v_addc_co_u32_e32 v3, vcc, 0, v163, vcc
	v_add_co_u32_e32 v6, vcc, s1, v162
	s_mov_b32 s1, 0x1e000
	s_nop 0
	v_addc_co_u32_e32 v7, vcc, 0, v163, vcc
	v_add_co_u32_e32 v10, vcc, s41, v162
	global_load_dwordx4 v[2:5], v[2:3], off sc0 nt
	s_nop 0
	global_load_dwordx4 v[6:9], v[6:7], off sc0 nt
	v_addc_co_u32_e32 v11, vcc, 0, v163, vcc
	v_add_co_u32_e32 v12, vcc, s1, v162
	s_mov_b32 s1, 0x200000
	s_nop 0
	v_addc_co_u32_e32 v13, vcc, 0, v163, vcc
	global_load_dwordx4 v[14:17], v[10:11], off sc0 nt
	global_load_dwordx4 v[26:29], v[12:13], off sc0 nt
	v_add_co_u32_e32 v10, vcc, s1, v162
	s_mov_b32 s1, 0x202000
	s_nop 0
	v_addc_co_u32_e32 v11, vcc, 0, v163, vcc
	v_add_co_u32_e32 v12, vcc, s1, v162
	s_mov_b32 s1, 0x204000
	s_nop 0
	v_addc_co_u32_e32 v13, vcc, 0, v163, vcc
	global_load_dwordx4 v[98:101], v[10:11], off sc0 nt
	global_load_dwordx4 v[106:109], v[12:13], off sc0 nt
	v_add_co_u32_e32 v10, vcc, s1, v162
	s_mov_b32 s1, 0x206000
	s_nop 0
	v_addc_co_u32_e32 v11, vcc, 0, v163, vcc
	v_add_co_u32_e32 v12, vcc, s1, v162
	s_mov_b32 s1, 0x208000
	s_nop 0
	v_addc_co_u32_e32 v13, vcc, 0, v163, vcc
	global_load_dwordx4 v[122:125], v[10:11], off sc0 nt
	global_load_dwordx4 v[126:129], v[12:13], off sc0 nt
	v_add_co_u32_e32 v10, vcc, s1, v162
	s_mov_b32 s1, 0x20a000
	s_nop 0
	v_addc_co_u32_e32 v11, vcc, 0, v163, vcc
	v_add_co_u32_e32 v12, vcc, s1, v162
	s_mov_b32 s1, 0x20c000
	s_nop 0
	v_addc_co_u32_e32 v13, vcc, 0, v163, vcc
	global_load_dwordx4 v[66:69], v[10:11], off sc0 nt
	global_load_dwordx4 v[74:77], v[12:13], off sc0 nt
	v_add_co_u32_e32 v10, vcc, s1, v162
	s_mov_b32 s1, 0x20e000
	s_nop 0
	v_addc_co_u32_e32 v11, vcc, 0, v163, vcc
	v_add_co_u32_e32 v12, vcc, s1, v162
	s_mov_b32 s1, 0x210000
	s_nop 0
	v_addc_co_u32_e32 v13, vcc, 0, v163, vcc
	global_load_dwordx4 v[102:105], v[10:11], off sc0 nt
	global_load_dwordx4 v[110:113], v[12:13], off sc0 nt
	v_add_co_u32_e32 v10, vcc, s1, v162
	s_mov_b32 s1, 0x212000
	s_nop 0
	v_addc_co_u32_e32 v11, vcc, 0, v163, vcc
	v_add_co_u32_e32 v12, vcc, s1, v162
	s_mov_b32 s1, 0x214000
	s_nop 0
	v_addc_co_u32_e32 v13, vcc, 0, v163, vcc
	global_load_dwordx4 v[34:37], v[10:11], off sc0 nt
	global_load_dwordx4 v[42:45], v[12:13], off sc0 nt
	v_add_co_u32_e32 v10, vcc, s1, v162
	s_mov_b32 s1, 0x216000
	s_nop 0
	v_addc_co_u32_e32 v11, vcc, 0, v163, vcc
	v_add_co_u32_e32 v12, vcc, s1, v162
	s_mov_b32 s1, 0x218000
	s_nop 0
	v_addc_co_u32_e32 v13, vcc, 0, v163, vcc
	global_load_dwordx4 v[70:73], v[10:11], off sc0 nt
	global_load_dwordx4 v[78:81], v[12:13], off sc0 nt
	v_add_co_u32_e32 v10, vcc, s1, v162
	s_mov_b32 s1, 0x21a000
	s_nop 0
	v_addc_co_u32_e32 v11, vcc, 0, v163, vcc
	v_add_co_u32_e32 v18, vcc, s1, v162
	s_mov_b32 s1, 0x21c000
	s_nop 0
	v_addc_co_u32_e32 v19, vcc, 0, v163, vcc
	v_add_co_u32_e32 v38, vcc, s1, v162
	s_mov_b32 s1, 0x21e000
	s_nop 0
	v_addc_co_u32_e32 v39, vcc, 0, v163, vcc
	v_add_co_u32_e32 v50, vcc, s1, v162
	global_load_dwordx4 v[10:13], v[10:11], off sc0 nt
	s_nop 0
	global_load_dwordx4 v[18:21], v[18:19], off sc0 nt
	v_addc_co_u32_e32 v51, vcc, 0, v163, vcc
	global_load_dwordx4 v[38:41], v[38:39], off sc0 nt
	s_nop 0
	global_load_dwordx4 v[50:53], v[50:51], off sc0 nt
	s_waitcnt vmcnt(0)
	v_mul_f32_e32 v86, 0x43800000, v86
	s_waitcnt vmcnt(30)
	v_mul_f32_e32 v94, 0x43800000, v94
	s_waitcnt vmcnt(27)
	v_mul_f32_e32 v54, 0x43800000, v54
	s_waitcnt vmcnt(26)
	v_mul_f32_e32 v62, 0x43800000, v62
	s_waitcnt vmcnt(23)
	v_mul_f32_e32 v22, 0x43800000, v22
	s_waitcnt vmcnt(22)
	v_mul_f32_e32 v30, 0x43800000, v30
	s_waitcnt vmcnt(19)
	v_mul_f32_e32 v2, 0x43800000, v2
	s_waitcnt vmcnt(18)
	v_mul_f32_e32 v6, 0x43800000, v6
	v_med3_f32 v86, v86, s85, v252
	v_med3_f32 v94, v94, s85, v252
	v_mov_b32_e32 v132, v155
	v_med3_f32 v54, v54, s85, v252
	v_med3_f32 v62, v62, s85, v252
	v_mov_b32_e32 v133, v155
	v_med3_f32 v22, v22, s85, v252
	v_med3_f32 v30, v30, s85, v252
	v_mov_b32_e32 v134, v155
	v_med3_f32 v2, v2, s85, v252
	v_med3_f32 v6, v6, s85, v252
	v_mov_b32_e32 v135, v155
	v_cvt_pk_fp8_f32 v132, v86, v94
	v_cvt_pk_fp8_f32 v133, v54, v62
	v_cvt_pk_fp8_f32 v134, v22, v30
	v_cvt_pk_fp8_f32 v135, v2, v6
	v_mul_f32_e32 v114, 0x43800000, v114
	v_mul_f32_e32 v118, 0x43800000, v118
	v_mul_f32_e32 v82, 0x43800000, v82
	v_mul_f32_e32 v86, 0x43800000, v90
	v_mul_f32_e32 v46, 0x43800000, v46
	v_mul_f32_e32 v54, 0x43800000, v58
	s_waitcnt vmcnt(17)
	v_mul_f32_e32 v14, 0x43800000, v14
	s_waitcnt vmcnt(16)
	v_mul_f32_e32 v22, 0x43800000, v26
	v_med3_f32 v114, v114, s85, v252
	v_med3_f32 v118, v118, s85, v252
	v_med3_f32 v82, v82, s85, v252
	v_med3_f32 v86, v86, s85, v252
	v_med3_f32 v46, v46, s85, v252
	v_med3_f32 v54, v54, s85, v252
	v_med3_f32 v14, v14, s85, v252
	v_med3_f32 v22, v22, s85, v252
	v_cvt_pk_fp8_f32 v132, v114, v118 op_sel:[0,0,1]
	v_cvt_pk_fp8_f32 v133, v82, v86 op_sel:[0,0,1]
	v_cvt_pk_fp8_f32 v134, v46, v54 op_sel:[0,0,1]
	v_cvt_pk_fp8_f32 v135, v14, v22 op_sel:[0,0,1]
	s_add_i32 s0, s0, 0
	v_mul_u32_u24_e32 v2, 0x110, v136
	v_add3_u32 v164, s0, v131, v2
	v_mul_f32_e32 v2, 0x43800000, v87
	v_mul_f32_e32 v6, 0x43800000, v95
	ds_write_b128 v164, v[132:135]
	v_med3_f32 v2, v2, s85, v252
	v_med3_f32 v6, v6, s85, v252
	v_mov_b32_e32 v132, v155
	v_cvt_pk_fp8_f32 v132, v2, v6
	v_mul_f32_e32 v2, 0x43800000, v55
	v_mul_f32_e32 v6, 0x43800000, v63
	v_med3_f32 v2, v2, s85, v252
	v_med3_f32 v6, v6, s85, v252
	v_mov_b32_e32 v133, v155
	v_cvt_pk_fp8_f32 v133, v2, v6
	v_mul_f32_e32 v2, 0x43800000, v23
	v_mul_f32_e32 v6, 0x43800000, v31
	v_med3_f32 v2, v2, s85, v252
	v_med3_f32 v6, v6, s85, v252
	v_mov_b32_e32 v134, v155
	v_mul_f32_e32 v14, 0x43800000, v115
	v_mul_f32_e32 v22, 0x43800000, v119
	v_cvt_pk_fp8_f32 v134, v2, v6
	v_mul_f32_e32 v2, 0x43800000, v3
	v_mul_f32_e32 v3, 0x43800000, v7
	v_med3_f32 v14, v14, s85, v252
	v_med3_f32 v22, v22, s85, v252
	v_med3_f32 v2, v2, s85, v252
	v_med3_f32 v3, v3, s85, v252
	v_mov_b32_e32 v135, v155
	v_cvt_pk_fp8_f32 v132, v14, v22 op_sel:[0,0,1]
	v_mul_f32_e32 v14, 0x43800000, v83
	v_mul_f32_e32 v22, 0x43800000, v91
	v_cvt_pk_fp8_f32 v135, v2, v3
	v_med3_f32 v14, v14, s85, v252
	v_med3_f32 v22, v22, s85, v252
	v_cvt_pk_fp8_f32 v133, v14, v22 op_sel:[0,0,1]
	v_mul_f32_e32 v14, 0x43800000, v47
	v_mul_f32_e32 v22, 0x43800000, v59
	v_mul_f32_e32 v6, 0x43800000, v15
	v_mul_f32_e32 v7, 0x43800000, v27
	v_med3_f32 v14, v14, s85, v252
	v_med3_f32 v22, v22, s85, v252
	v_med3_f32 v6, v6, s85, v252
	v_med3_f32 v7, v7, s85, v252
	v_cvt_pk_fp8_f32 v134, v14, v22 op_sel:[0,0,1]
	v_cvt_pk_fp8_f32 v135, v6, v7 op_sel:[0,0,1]
	v_mul_f32_e32 v2, 0x43800000, v88
	v_mul_f32_e32 v3, 0x43800000, v96
	v_med3_f32 v2, v2, s85, v252
	ds_write_b128 v164, v[132:135] offset:272
	v_med3_f32 v3, v3, s85, v252
	v_mov_b32_e32 v132, v155
	v_cvt_pk_fp8_f32 v132, v2, v3
	v_mul_f32_e32 v2, 0x43800000, v56
	v_mul_f32_e32 v3, 0x43800000, v64
	v_med3_f32 v2, v2, s85, v252
	v_med3_f32 v3, v3, s85, v252
	v_mov_b32_e32 v133, v155
	v_mul_f32_e32 v6, 0x43800000, v116
	v_mul_f32_e32 v7, 0x43800000, v120
	v_cvt_pk_fp8_f32 v133, v2, v3
	v_mul_f32_e32 v2, 0x43800000, v24
	v_mul_f32_e32 v3, 0x43800000, v32
	v_med3_f32 v6, v6, s85, v252
	v_med3_f32 v7, v7, s85, v252
	v_med3_f32 v2, v2, s85, v252
	v_med3_f32 v3, v3, s85, v252
	v_mov_b32_e32 v134, v155
	v_cvt_pk_fp8_f32 v132, v6, v7 op_sel:[0,0,1]
	v_mul_f32_e32 v6, 0x43800000, v84
	v_mul_f32_e32 v7, 0x43800000, v92
	v_cvt_pk_fp8_f32 v134, v2, v3
	v_med3_f32 v6, v6, s85, v252
	v_med3_f32 v7, v7, s85, v252
	v_mul_f32_e32 v2, 0x43800000, v4
	v_mul_f32_e32 v3, 0x43800000, v8
	v_cvt_pk_fp8_f32 v133, v6, v7 op_sel:[0,0,1]
	v_mul_f32_e32 v6, 0x43800000, v48
	v_mul_f32_e32 v7, 0x43800000, v60
	v_med3_f32 v2, v2, s85, v252
	v_med3_f32 v3, v3, s85, v252
	v_mov_b32_e32 v135, v155
	v_med3_f32 v6, v6, s85, v252
	v_med3_f32 v7, v7, s85, v252
	v_cvt_pk_fp8_f32 v135, v2, v3
	v_mul_f32_e32 v2, 0x43800000, v89
	v_mul_f32_e32 v3, 0x43800000, v97
	v_cvt_pk_fp8_f32 v134, v6, v7 op_sel:[0,0,1]
	v_med3_f32 v7, v2, s85, v252
	v_med3_f32 v3, v3, s85, v252
	v_mov_b32_e32 v2, v155
	v_mul_f32_e32 v4, 0x43800000, v16
	v_mul_f32_e32 v6, 0x43800000, v28
	v_cvt_pk_fp8_f32 v2, v7, v3
	v_med3_f32 v4, v4, s85, v252
	v_med3_f32 v6, v6, s85, v252
	v_cvt_pk_fp8_f32 v135, v4, v6 op_sel:[0,0,1]
	v_mul_f32_e32 v4, 0x43800000, v117
	v_mul_f32_e32 v6, 0x43800000, v121
	v_med3_f32 v4, v4, s85, v252
	v_med3_f32 v6, v6, s85, v252
	v_cvt_pk_fp8_f32 v2, v4, v6 op_sel:[0,0,1]
	v_mul_f32_e32 v3, 0x43800000, v57
	v_mul_f32_e32 v4, 0x43800000, v65
	v_med3_f32 v8, v3, s85, v252
	v_med3_f32 v4, v4, s85, v252
	v_mov_b32_e32 v3, v155
	v_cvt_pk_fp8_f32 v3, v8, v4
	v_mul_f32_e32 v6, 0x43800000, v85
	v_mul_f32_e32 v7, 0x43800000, v93
	v_med3_f32 v6, v6, s85, v252
	v_med3_f32 v7, v7, s85, v252
	v_cvt_pk_fp8_f32 v3, v6, v7 op_sel:[0,0,1]
	v_mul_f32_e32 v4, 0x43800000, v25
	v_mul_f32_e32 v6, 0x43800000, v33
	v_med3_f32 v14, v4, s85, v252
	v_med3_f32 v6, v6, s85, v252
	v_mov_b32_e32 v4, v155
	v_cvt_pk_fp8_f32 v4, v14, v6
	v_mul_f32_e32 v5, 0x43800000, v5
	v_mul_f32_e32 v6, 0x43800000, v9
	v_med3_f32 v9, v5, s85, v252
	v_med3_f32 v6, v6, s85, v252
	v_mov_b32_e32 v5, v155
	v_mul_f32_e32 v7, 0x43800000, v49
	v_mul_f32_e32 v8, 0x43800000, v61
	v_cvt_pk_fp8_f32 v5, v9, v6
	v_med3_f32 v7, v7, s85, v252
	v_med3_f32 v8, v8, s85, v252
	v_cvt_pk_fp8_f32 v4, v7, v8 op_sel:[0,0,1]
	v_mul_f32_e32 v7, 0x43800000, v17
	v_mul_f32_e32 v8, 0x43800000, v29
	v_med3_f32 v7, v7, s85, v252
	v_med3_f32 v8, v8, s85, v252
	v_cvt_pk_fp8_f32 v5, v7, v8 op_sel:[0,0,1]
	ds_write_b128 v164, v[132:135] offset:544
	v_ashrrev_i32_e32 v132, 4, v130
	v_ashrrev_i32_e32 v133, 31, v132
	ds_write_b128 v164, v[2:5] offset:816
	v_lshlrev_b32_e32 v2, 4, v130
	v_and_b32_e32 v154, 0xf0, v2
	v_add_u32_e32 v2, 0x200, v130
	v_ashrrev_i32_e32 v136, 4, v2
	v_add_u32_e32 v2, 0x400, v130
	v_ashrrev_i32_e32 v140, 4, v2
	v_add_u32_e32 v2, 0x600, v130
	v_ashrrev_i32_e32 v158, 4, v2
	v_ashrrev_i32_e32 v137, 31, v136
	v_ashrrev_i32_e32 v141, 31, v140
	v_ashrrev_i32_e32 v159, 31, v158
	s_waitcnt lgkmcnt(0)
	s_barrier
	v_lshlrev_b64 v[134:135], 11, v[132:133]
	v_lshlrev_b64 v[138:139], 11, v[136:137]
	v_lshlrev_b64 v[152:153], 11, v[140:141]
	v_lshlrev_b64 v[160:161], 11, v[158:159]
	v_add_co_u32_e32 v2, vcc, s43, v162
	s_mov_b32 s0, 0x402000
	s_nop 0
	v_addc_co_u32_e32 v3, vcc, 0, v163, vcc
	v_add_co_u32_e32 v4, vcc, s0, v162
	s_mov_b32 s0, 0x406000
	s_nop 0
	v_addc_co_u32_e32 v5, vcc, 0, v163, vcc
	global_load_dwordx4 v[86:89], v[2:3], off sc0 nt
	global_load_dwordx4 v[94:97], v[4:5], off sc0 nt
	v_add_co_u32_e32 v2, vcc, s44, v162
	s_nop 1
	v_addc_co_u32_e32 v3, vcc, 0, v163, vcc
	v_add_co_u32_e32 v4, vcc, s0, v162
	s_mov_b32 s0, 0x40a000
	s_nop 0
	v_addc_co_u32_e32 v5, vcc, 0, v163, vcc
	global_load_dwordx4 v[114:117], v[2:3], off sc0 nt
	global_load_dwordx4 v[118:121], v[4:5], off sc0 nt
	v_add_co_u32_e32 v2, vcc, s45, v162
	s_nop 1
	v_addc_co_u32_e32 v3, vcc, 0, v163, vcc
	v_add_co_u32_e32 v4, vcc, s0, v162
	s_mov_b32 s0, 0x40e000
	s_nop 0
	v_addc_co_u32_e32 v5, vcc, 0, v163, vcc
	global_load_dwordx4 v[54:57], v[2:3], off sc0 nt
	global_load_dwordx4 v[62:65], v[4:5], off sc0 nt
	v_add_co_u32_e32 v2, vcc, s46, v162
	s_nop 1
	v_addc_co_u32_e32 v3, vcc, 0, v163, vcc
	v_add_co_u32_e32 v4, vcc, s0, v162
	s_mov_b32 s0, 0x412000
	s_nop 0
	v_addc_co_u32_e32 v5, vcc, 0, v163, vcc
	global_load_dwordx4 v[82:85], v[2:3], off sc0 nt
	global_load_dwordx4 v[90:93], v[4:5], off sc0 nt
	v_add_co_u32_e32 v2, vcc, s47, v162
	s_nop 1
	v_addc_co_u32_e32 v3, vcc, 0, v163, vcc
	v_add_co_u32_e32 v4, vcc, s0, v162
	s_mov_b32 s0, 0x416000
	s_nop 0
	v_addc_co_u32_e32 v5, vcc, 0, v163, vcc
	global_load_dwordx4 v[22:25], v[2:3], off sc0 nt
	global_load_dwordx4 v[30:33], v[4:5], off sc0 nt
	v_add_co_u32_e32 v2, vcc, s48, v162
	s_nop 1
	v_addc_co_u32_e32 v3, vcc, 0, v163, vcc
	v_add_co_u32_e32 v4, vcc, s0, v162
	s_mov_b32 s0, 0x41a000
	s_nop 0
	v_addc_co_u32_e32 v5, vcc, 0, v163, vcc
	global_load_dwordx4 v[46:49], v[2:3], off sc0 nt
	global_load_dwordx4 v[58:61], v[4:5], off sc0 nt
	v_add_co_u32_e32 v2, vcc, s49, v162
	s_nop 1
	v_addc_co_u32_e32 v3, vcc, 0, v163, vcc
	v_add_co_u32_e32 v6, vcc, s0, v162
	s_mov_b32 s0, 0x41e000
	s_nop 0
	v_addc_co_u32_e32 v7, vcc, 0, v163, vcc
	v_add_co_u32_e32 v14, vcc, s52, v162
	global_load_dwordx4 v[2:5], v[2:3], off sc0 nt
	s_nop 0
	global_load_dwordx4 v[6:9], v[6:7], off sc0 nt
	v_addc_co_u32_e32 v15, vcc, 0, v163, vcc
	v_add_co_u32_e32 v26, vcc, s0, v162
	s_nop 1
	v_addc_co_u32_e32 v27, vcc, 0, v163, vcc
	global_load_dwordx4 v[14:17], v[14:15], off sc0 nt
	s_nop 0
	global_load_dwordx4 v[26:29], v[26:27], off sc0 nt
	v_add_u32_e32 v166, 0, v154
	v_mad_u64_u32 v[142:143], s[0:1], v132, s42, v[166:167]
	ds_read_b128 v[130:133], v142
	v_lshl_add_u64 v[168:169], s[30:31], 0, v[154:155]
	v_lshl_add_u64 v[144:145], v[168:169], 0, v[134:135]
	v_mad_u64_u32 v[146:147], s[0:1], v136, s42, v[166:167]
	s_waitcnt lgkmcnt(0)
	global_store_dwordx4 v[144:145], v[130:133], off nt
	ds_read_b128 v[130:133], v146
	v_lshl_add_u64 v[148:149], v[168:169], 0, v[138:139]
	v_mad_u64_u32 v[150:151], s[0:1], v140, s42, v[166:167]
	v_lshl_add_u64 v[152:153], v[168:169], 0, v[152:153]
	s_waitcnt lgkmcnt(0)
	global_store_dwordx4 v[148:149], v[130:133], off nt
	ds_read_b128 v[130:133], v150
	v_mad_u64_u32 v[158:159], s[0:1], v158, s42, v[166:167]
	v_lshl_add_u64 v[160:161], v[168:169], 0, v[160:161]
	s_waitcnt lgkmcnt(0)
	global_store_dwordx4 v[152:153], v[130:133], off nt
	ds_read_b128 v[130:133], v158
	s_waitcnt lgkmcnt(0)
	global_store_dwordx4 v[160:161], v[130:133], off nt
	s_waitcnt vmcnt(35)
	v_mul_f32_e32 v98, 0x43800000, v98
	s_waitcnt vmcnt(34)
	v_mul_f32_e32 v106, 0x43800000, v106
	s_waitcnt vmcnt(31)
	v_mul_f32_e32 v66, 0x43800000, v66
	s_waitcnt vmcnt(30)
	v_mul_f32_e32 v74, 0x43800000, v74
	s_waitcnt vmcnt(27)
	v_mul_f32_e32 v34, 0x43800000, v34
	s_waitcnt vmcnt(26)
	v_mul_f32_e32 v42, 0x43800000, v42
	s_waitcnt vmcnt(23)
	v_mul_f32_e32 v10, 0x43800000, v10
	s_waitcnt vmcnt(22)
	v_mul_f32_e32 v18, 0x43800000, v18
	v_med3_f32 v98, v98, s85, v252
	v_med3_f32 v106, v106, s85, v252
	v_mov_b32_e32 v130, v155
	v_med3_f32 v66, v66, s85, v252
	v_med3_f32 v74, v74, s85, v252
	v_mov_b32_e32 v131, v155
	v_med3_f32 v34, v34, s85, v252
	v_med3_f32 v42, v42, s85, v252
	v_mov_b32_e32 v132, v155
	v_med3_f32 v10, v10, s85, v252
	v_med3_f32 v18, v18, s85, v252
	v_mov_b32_e32 v133, v155
	v_cvt_pk_fp8_f32 v130, v98, v106
	v_cvt_pk_fp8_f32 v131, v66, v74
	v_cvt_pk_fp8_f32 v132, v34, v42
	v_cvt_pk_fp8_f32 v133, v10, v18
	v_mul_f32_e32 v122, 0x43800000, v122
	v_mul_f32_e32 v126, 0x43800000, v126
	v_mul_f32_e32 v98, 0x43800000, v102
	v_mul_f32_e32 v102, 0x43800000, v110
	v_mul_f32_e32 v66, 0x43800000, v70
	v_mul_f32_e32 v70, 0x43800000, v78
	s_waitcnt vmcnt(21)
	v_mul_f32_e32 v34, 0x43800000, v38
	s_waitcnt vmcnt(20)
	v_mul_f32_e32 v38, 0x43800000, v50
	v_med3_f32 v122, v122, s85, v252
	v_med3_f32 v126, v126, s85, v252
	v_med3_f32 v98, v98, s85, v252
	v_med3_f32 v102, v102, s85, v252
	v_med3_f32 v66, v66, s85, v252
	v_med3_f32 v70, v70, s85, v252
	v_med3_f32 v34, v34, s85, v252
	v_med3_f32 v38, v38, s85, v252
	v_cvt_pk_fp8_f32 v130, v122, v126 op_sel:[0,0,1]
	v_cvt_pk_fp8_f32 v131, v98, v102 op_sel:[0,0,1]
	v_cvt_pk_fp8_f32 v132, v66, v70 op_sel:[0,0,1]
	v_cvt_pk_fp8_f32 v133, v34, v38 op_sel:[0,0,1]
	v_mul_f32_e32 v10, 0x43800000, v99
	v_mul_f32_e32 v18, 0x43800000, v107
	v_med3_f32 v10, v10, s85, v252
	ds_write_b128 v164, v[130:133] offset:34816
	v_med3_f32 v18, v18, s85, v252
	v_mov_b32_e32 v130, v155
	v_cvt_pk_fp8_f32 v130, v10, v18
	v_mul_f32_e32 v10, 0x43800000, v67
	v_mul_f32_e32 v18, 0x43800000, v75
	v_med3_f32 v10, v10, s85, v252
	v_med3_f32 v18, v18, s85, v252
	v_mov_b32_e32 v131, v155
	v_cvt_pk_fp8_f32 v131, v10, v18
	v_mul_f32_e32 v10, 0x43800000, v35
	v_mul_f32_e32 v18, 0x43800000, v43
	v_med3_f32 v10, v10, s85, v252
	v_med3_f32 v18, v18, s85, v252
	v_mov_b32_e32 v132, v155
	v_mul_f32_e32 v34, 0x43800000, v123
	v_mul_f32_e32 v38, 0x43800000, v127
	v_cvt_pk_fp8_f32 v132, v10, v18
	v_mul_f32_e32 v10, 0x43800000, v11
	v_mul_f32_e32 v11, 0x43800000, v19
	v_med3_f32 v34, v34, s85, v252
	v_med3_f32 v38, v38, s85, v252
	v_med3_f32 v10, v10, s85, v252
	v_med3_f32 v11, v11, s85, v252
	v_mov_b32_e32 v133, v155
	v_cvt_pk_fp8_f32 v130, v34, v38 op_sel:[0,0,1]
	v_mul_f32_e32 v34, 0x43800000, v103
	v_mul_f32_e32 v38, 0x43800000, v111
	v_cvt_pk_fp8_f32 v133, v10, v11
	v_med3_f32 v34, v34, s85, v252
	v_med3_f32 v38, v38, s85, v252
	v_cvt_pk_fp8_f32 v131, v34, v38 op_sel:[0,0,1]
	v_mul_f32_e32 v34, 0x43800000, v71
	v_mul_f32_e32 v35, 0x43800000, v79
	v_mul_f32_e32 v18, 0x43800000, v39
	v_mul_f32_e32 v19, 0x43800000, v51
	v_med3_f32 v34, v34, s85, v252
	v_med3_f32 v35, v35, s85, v252
	v_med3_f32 v18, v18, s85, v252
	v_med3_f32 v19, v19, s85, v252
	v_cvt_pk_fp8_f32 v132, v34, v35 op_sel:[0,0,1]
	v_cvt_pk_fp8_f32 v133, v18, v19 op_sel:[0,0,1]
	v_mul_f32_e32 v10, 0x43800000, v100
	v_mul_f32_e32 v11, 0x43800000, v108
	v_med3_f32 v10, v10, s85, v252
	ds_write_b128 v164, v[130:133] offset:35088
	v_med3_f32 v11, v11, s85, v252
	v_mov_b32_e32 v130, v155
	v_cvt_pk_fp8_f32 v130, v10, v11
	v_mul_f32_e32 v10, 0x43800000, v68
	v_mul_f32_e32 v11, 0x43800000, v76
	v_med3_f32 v10, v10, s85, v252
	v_med3_f32 v11, v11, s85, v252
	v_mov_b32_e32 v131, v155
	v_mul_f32_e32 v18, 0x43800000, v124
	v_mul_f32_e32 v19, 0x43800000, v128
	v_cvt_pk_fp8_f32 v131, v10, v11
	v_mul_f32_e32 v10, 0x43800000, v36
	v_mul_f32_e32 v11, 0x43800000, v44
	v_med3_f32 v18, v18, s85, v252
	v_med3_f32 v19, v19, s85, v252
	v_med3_f32 v10, v10, s85, v252
	v_med3_f32 v11, v11, s85, v252
	v_mov_b32_e32 v132, v155
	v_cvt_pk_fp8_f32 v130, v18, v19 op_sel:[0,0,1]
	v_mul_f32_e32 v18, 0x43800000, v104
	v_mul_f32_e32 v19, 0x43800000, v112
	v_cvt_pk_fp8_f32 v132, v10, v11
	v_med3_f32 v18, v18, s85, v252
	v_med3_f32 v19, v19, s85, v252
	v_mul_f32_e32 v10, 0x43800000, v12
	v_mul_f32_e32 v11, 0x43800000, v20
	v_cvt_pk_fp8_f32 v131, v18, v19 op_sel:[0,0,1]
	v_mul_f32_e32 v18, 0x43800000, v72
	v_mul_f32_e32 v19, 0x43800000, v80
	v_med3_f32 v10, v10, s85, v252
	v_med3_f32 v11, v11, s85, v252
	v_mov_b32_e32 v133, v155
	v_med3_f32 v18, v18, s85, v252
	v_med3_f32 v19, v19, s85, v252
	v_cvt_pk_fp8_f32 v133, v10, v11
	v_mul_f32_e32 v10, 0x43800000, v101
	v_mul_f32_e32 v11, 0x43800000, v109
	v_cvt_pk_fp8_f32 v132, v18, v19 op_sel:[0,0,1]
	v_med3_f32 v19, v10, s85, v252
	v_med3_f32 v11, v11, s85, v252
	v_mov_b32_e32 v10, v155
	v_mul_f32_e32 v12, 0x43800000, v40
	v_mul_f32_e32 v18, 0x43800000, v52
	v_cvt_pk_fp8_f32 v10, v19, v11
	v_med3_f32 v12, v12, s85, v252
	v_med3_f32 v18, v18, s85, v252
	v_cvt_pk_fp8_f32 v133, v12, v18 op_sel:[0,0,1]
	v_mul_f32_e32 v12, 0x43800000, v125
	v_mul_f32_e32 v18, 0x43800000, v129
	v_med3_f32 v12, v12, s85, v252
	v_med3_f32 v18, v18, s85, v252
	v_cvt_pk_fp8_f32 v10, v12, v18 op_sel:[0,0,1]
	v_mul_f32_e32 v11, 0x43800000, v69
	v_mul_f32_e32 v12, 0x43800000, v77
	v_med3_f32 v20, v11, s85, v252
	v_med3_f32 v12, v12, s85, v252
	v_mov_b32_e32 v11, v155
	v_cvt_pk_fp8_f32 v11, v20, v12
	v_mul_f32_e32 v18, 0x43800000, v105
	v_mul_f32_e32 v19, 0x43800000, v113
	v_med3_f32 v18, v18, s85, v252
	v_med3_f32 v19, v19, s85, v252
	v_cvt_pk_fp8_f32 v11, v18, v19 op_sel:[0,0,1]
	v_mul_f32_e32 v12, 0x43800000, v37
	v_mul_f32_e32 v18, 0x43800000, v45
	v_med3_f32 v34, v12, s85, v252
	v_med3_f32 v18, v18, s85, v252
	v_mov_b32_e32 v12, v155
	v_cvt_pk_fp8_f32 v12, v34, v18
	v_mul_f32_e32 v13, 0x43800000, v13
	v_mul_f32_e32 v18, 0x43800000, v21
	v_med3_f32 v21, v13, s85, v252
	v_med3_f32 v18, v18, s85, v252
	v_mov_b32_e32 v13, v155
	v_mul_f32_e32 v19, 0x43800000, v73
	v_mul_f32_e32 v20, 0x43800000, v81
	v_cvt_pk_fp8_f32 v13, v21, v18
	v_med3_f32 v19, v19, s85, v252
	v_med3_f32 v20, v20, s85, v252
	v_cvt_pk_fp8_f32 v12, v19, v20 op_sel:[0,0,1]
	v_mul_f32_e32 v19, 0x43800000, v41
	v_mul_f32_e32 v20, 0x43800000, v53
	v_med3_f32 v19, v19, s85, v252
	v_med3_f32 v20, v20, s85, v252
	v_cvt_pk_fp8_f32 v13, v19, v20 op_sel:[0,0,1]
	ds_write_b128 v164, v[130:133] offset:35360
	ds_write_b128 v164, v[10:13] offset:35632
	s_waitcnt lgkmcnt(0)
	s_barrier
	s_mov_b32 s0, 0x600000
	v_add_co_u32_e32 v10, vcc, s0, v162
	s_mov_b32 s0, 0x602000
	s_nop 0
	v_addc_co_u32_e32 v11, vcc, 0, v163, vcc
	v_add_co_u32_e32 v12, vcc, s0, v162
	s_mov_b32 s0, 0x604000
	s_nop 0
	v_addc_co_u32_e32 v13, vcc, 0, v163, vcc
	global_load_dwordx4 v[106:109], v[10:11], off sc0 nt
	global_load_dwordx4 v[122:125], v[12:13], off sc0 nt
	v_add_co_u32_e32 v10, vcc, s0, v162
	s_mov_b32 s0, 0x606000
	s_nop 0
	v_addc_co_u32_e32 v11, vcc, 0, v163, vcc
	v_add_co_u32_e32 v12, vcc, s0, v162
	s_mov_b32 s0, 0x608000
	s_nop 0
	v_addc_co_u32_e32 v13, vcc, 0, v163, vcc
	global_load_dwordx4 v[130:133], v[10:11], off sc0 nt
	global_load_dwordx4 v[138:141], v[12:13], off sc0 nt
	v_add_co_u32_e32 v10, vcc, s0, v162
	s_mov_b32 s0, 0x60a000
	s_nop 0
	v_addc_co_u32_e32 v11, vcc, 0, v163, vcc
	v_add_co_u32_e32 v12, vcc, s0, v162
	s_mov_b32 s0, 0x60c000
	s_nop 0
	v_addc_co_u32_e32 v13, vcc, 0, v163, vcc
	global_load_dwordx4 v[74:77], v[10:11], off sc0 nt
	global_load_dwordx4 v[98:101], v[12:13], off sc0 nt
	v_add_co_u32_e32 v10, vcc, s0, v162
	s_mov_b32 s0, 0x60e000
	s_nop 0
	v_addc_co_u32_e32 v11, vcc, 0, v163, vcc
	v_add_co_u32_e32 v12, vcc, s0, v162
	s_mov_b32 s0, 0x610000
	s_nop 0
	v_addc_co_u32_e32 v13, vcc, 0, v163, vcc
	global_load_dwordx4 v[110:113], v[10:11], off sc0 nt
	global_load_dwordx4 v[126:129], v[12:13], off sc0 nt
	v_add_co_u32_e32 v10, vcc, s0, v162
	s_mov_b32 s0, 0x612000
	s_nop 0
	v_addc_co_u32_e32 v11, vcc, 0, v163, vcc
	v_add_co_u32_e32 v12, vcc, s0, v162
	s_mov_b32 s0, 0x614000
	s_nop 0
	v_addc_co_u32_e32 v13, vcc, 0, v163, vcc
	global_load_dwordx4 v[38:41], v[10:11], off sc0 nt
	global_load_dwordx4 v[50:53], v[12:13], off sc0 nt
	v_add_co_u32_e32 v10, vcc, s0, v162
	s_mov_b32 s0, 0x616000
	s_nop 0
	v_addc_co_u32_e32 v11, vcc, 0, v163, vcc
	v_add_co_u32_e32 v12, vcc, s0, v162
	s_mov_b32 s0, 0x618000
	s_nop 0
	v_addc_co_u32_e32 v13, vcc, 0, v163, vcc
	global_load_dwordx4 v[78:81], v[10:11], off sc0 nt
	global_load_dwordx4 v[102:105], v[12:13], off sc0 nt
	v_add_co_u32_e32 v10, vcc, s0, v162
	s_mov_b32 s0, 0x61a000
	s_nop 0
	v_addc_co_u32_e32 v11, vcc, 0, v163, vcc
	v_add_co_u32_e32 v18, vcc, s0, v162
	s_mov_b32 s0, 0x61c000
	s_nop 0
	v_addc_co_u32_e32 v19, vcc, 0, v163, vcc
	v_add_co_u32_e32 v34, vcc, s0, v162
	s_mov_b32 s0, 0x61e000
	s_nop 0
	v_addc_co_u32_e32 v35, vcc, 0, v163, vcc
	v_add_co_u32_e32 v36, vcc, s0, v162
	global_load_dwordx4 v[10:13], v[10:11], off sc0 nt
	s_nop 0
	global_load_dwordx4 v[18:21], v[18:19], off sc0 nt
	v_addc_co_u32_e32 v37, vcc, 0, v163, vcc
	global_load_dwordx4 v[42:45], v[34:35], off sc0 nt
	global_load_dwordx4 v[66:69], v[36:37], off sc0 nt
	ds_read_b128 v[34:37], v142 offset:34816
	s_waitcnt lgkmcnt(0)
	global_store_dwordx4 v[144:145], v[34:37], off offset:256 nt
	ds_read_b128 v[34:37], v146 offset:34816
	s_waitcnt lgkmcnt(0)
	global_store_dwordx4 v[148:149], v[34:37], off offset:256 nt
	ds_read_b128 v[34:37], v150 offset:34816
	s_waitcnt lgkmcnt(0)
	global_store_dwordx4 v[152:153], v[34:37], off offset:256 nt
	ds_read_b128 v[34:37], v158 offset:34816
	s_waitcnt lgkmcnt(0)
	global_store_dwordx4 v[160:161], v[34:37], off offset:256 nt
	s_waitcnt vmcnt(39)
	s_nop 0
	v_mul_f32_e32 v34, 0x43800000, v86
	s_waitcnt vmcnt(38)
	v_mul_f32_e32 v35, 0x43800000, v94
	v_med3_f32 v70, v34, s85, v252
	v_med3_f32 v35, v35, s85, v252
	v_mov_b32_e32 v34, v155
	v_cvt_pk_fp8_f32 v34, v70, v35
	s_waitcnt vmcnt(37)
	v_mul_f32_e32 v36, 0x43800000, v114
	s_waitcnt vmcnt(36)
	v_mul_f32_e32 v37, 0x43800000, v118
	v_med3_f32 v36, v36, s85, v252
	v_med3_f32 v37, v37, s85, v252
	v_cvt_pk_fp8_f32 v34, v36, v37 op_sel:[0,0,1]
	s_waitcnt vmcnt(35)
	v_mul_f32_e32 v35, 0x43800000, v54
	s_waitcnt vmcnt(34)
	v_mul_f32_e32 v36, 0x43800000, v62
	v_med3_f32 v62, v35, s85, v252
	v_med3_f32 v36, v36, s85, v252
	v_mov_b32_e32 v35, v155
	v_cvt_pk_fp8_f32 v35, v62, v36
	s_waitcnt vmcnt(31)
	v_mul_f32_e32 v22, 0x43800000, v22
	s_waitcnt vmcnt(30)
	v_mul_f32_e32 v30, 0x43800000, v30
	s_waitcnt vmcnt(29)
	v_mul_f32_e32 v36, 0x43800000, v46
	v_med3_f32 v22, v22, s85, v252
	v_med3_f32 v30, v30, s85, v252
	v_med3_f32 v46, v36, s85, v252
	v_mov_b32_e32 v36, v155
	v_mul_f32_e32 v37, 0x43800000, v82
	v_mul_f32_e32 v54, 0x43800000, v90
	v_cvt_pk_fp8_f32 v36, v22, v30
	v_med3_f32 v37, v37, s85, v252
	v_med3_f32 v54, v54, s85, v252
	v_cvt_pk_fp8_f32 v35, v37, v54 op_sel:[0,0,1]
	s_waitcnt vmcnt(28)
	v_mul_f32_e32 v37, 0x43800000, v58
	v_med3_f32 v37, v37, s85, v252
	s_waitcnt vmcnt(27)
	v_mul_f32_e32 v2, 0x43800000, v2
	s_waitcnt vmcnt(26)
	v_mul_f32_e32 v6, 0x43800000, v6
	v_cvt_pk_fp8_f32 v36, v46, v37 op_sel:[0,0,1]
	v_med3_f32 v2, v2, s85, v252
	v_med3_f32 v6, v6, s85, v252
	v_mov_b32_e32 v37, v155
	v_cvt_pk_fp8_f32 v37, v2, v6
	s_waitcnt vmcnt(25)
	v_mul_f32_e32 v14, 0x43800000, v14
	s_waitcnt vmcnt(24)
	v_mul_f32_e32 v22, 0x43800000, v26
	v_med3_f32 v14, v14, s85, v252
	v_med3_f32 v22, v22, s85, v252
	v_cvt_pk_fp8_f32 v37, v14, v22 op_sel:[0,0,1]
	v_mul_f32_e32 v2, 0x43800000, v87
	v_mul_f32_e32 v6, 0x43800000, v95
	v_med3_f32 v2, v2, s85, v252
	ds_write_b128 v164, v[34:37]
	v_med3_f32 v6, v6, s85, v252
	v_mov_b32_e32 v34, v155
	v_cvt_pk_fp8_f32 v34, v2, v6
	v_mul_f32_e32 v2, 0x43800000, v55
	v_mul_f32_e32 v6, 0x43800000, v63
	v_med3_f32 v2, v2, s85, v252
	v_med3_f32 v6, v6, s85, v252
	v_mov_b32_e32 v35, v155
	v_cvt_pk_fp8_f32 v35, v2, v6
	v_mul_f32_e32 v2, 0x43800000, v23
	v_mul_f32_e32 v6, 0x43800000, v31
	v_med3_f32 v2, v2, s85, v252
	v_med3_f32 v6, v6, s85, v252
	v_mov_b32_e32 v36, v155
	v_mul_f32_e32 v14, 0x43800000, v115
	v_mul_f32_e32 v22, 0x43800000, v119
	v_cvt_pk_fp8_f32 v36, v2, v6
	v_mul_f32_e32 v2, 0x43800000, v3
	v_mul_f32_e32 v3, 0x43800000, v7
	v_med3_f32 v14, v14, s85, v252
	v_med3_f32 v22, v22, s85, v252
	v_med3_f32 v2, v2, s85, v252
	v_med3_f32 v3, v3, s85, v252
	v_mov_b32_e32 v37, v155
	v_cvt_pk_fp8_f32 v34, v14, v22 op_sel:[0,0,1]
	v_mul_f32_e32 v14, 0x43800000, v83
	v_mul_f32_e32 v22, 0x43800000, v91
	v_cvt_pk_fp8_f32 v37, v2, v3
	v_med3_f32 v14, v14, s85, v252
	v_med3_f32 v22, v22, s85, v252
	v_cvt_pk_fp8_f32 v35, v14, v22 op_sel:[0,0,1]
	v_mul_f32_e32 v14, 0x43800000, v47
	v_mul_f32_e32 v22, 0x43800000, v59
	v_mul_f32_e32 v6, 0x43800000, v15
	v_mul_f32_e32 v7, 0x43800000, v27
	v_med3_f32 v14, v14, s85, v252
	v_med3_f32 v22, v22, s85, v252
	v_med3_f32 v6, v6, s85, v252
	v_med3_f32 v7, v7, s85, v252
	v_cvt_pk_fp8_f32 v36, v14, v22 op_sel:[0,0,1]
	v_cvt_pk_fp8_f32 v37, v6, v7 op_sel:[0,0,1]
	v_mul_f32_e32 v2, 0x43800000, v88
	v_mul_f32_e32 v3, 0x43800000, v96
	v_med3_f32 v2, v2, s85, v252
	ds_write_b128 v164, v[34:37] offset:272
	v_med3_f32 v3, v3, s85, v252
	v_mov_b32_e32 v34, v155
	v_cvt_pk_fp8_f32 v34, v2, v3
	v_mul_f32_e32 v2, 0x43800000, v56
	v_mul_f32_e32 v3, 0x43800000, v64
	v_med3_f32 v2, v2, s85, v252
	v_med3_f32 v3, v3, s85, v252
	v_mov_b32_e32 v35, v155
	v_mul_f32_e32 v6, 0x43800000, v116
	v_mul_f32_e32 v7, 0x43800000, v120
	v_cvt_pk_fp8_f32 v35, v2, v3
	v_mul_f32_e32 v2, 0x43800000, v24
	v_mul_f32_e32 v3, 0x43800000, v32
	v_med3_f32 v6, v6, s85, v252
	v_med3_f32 v7, v7, s85, v252
	v_med3_f32 v2, v2, s85, v252
	v_med3_f32 v3, v3, s85, v252
	v_mov_b32_e32 v36, v155
	v_cvt_pk_fp8_f32 v34, v6, v7 op_sel:[0,0,1]
	v_mul_f32_e32 v6, 0x43800000, v84
	v_mul_f32_e32 v7, 0x43800000, v92
	v_cvt_pk_fp8_f32 v36, v2, v3
	v_med3_f32 v6, v6, s85, v252
	v_med3_f32 v7, v7, s85, v252
	v_mul_f32_e32 v2, 0x43800000, v4
	v_mul_f32_e32 v3, 0x43800000, v8
	v_cvt_pk_fp8_f32 v35, v6, v7 op_sel:[0,0,1]
	v_mul_f32_e32 v6, 0x43800000, v48
	v_mul_f32_e32 v7, 0x43800000, v60
	v_med3_f32 v2, v2, s85, v252
	v_med3_f32 v3, v3, s85, v252
	v_mov_b32_e32 v37, v155
	v_med3_f32 v6, v6, s85, v252
	v_med3_f32 v7, v7, s85, v252
	v_cvt_pk_fp8_f32 v37, v2, v3
	v_mul_f32_e32 v2, 0x43800000, v89
	v_mul_f32_e32 v3, 0x43800000, v97
	v_cvt_pk_fp8_f32 v36, v6, v7 op_sel:[0,0,1]
	v_med3_f32 v7, v2, s85, v252
	v_med3_f32 v3, v3, s85, v252
	v_mov_b32_e32 v2, v155
	v_mul_f32_e32 v4, 0x43800000, v16
	v_mul_f32_e32 v6, 0x43800000, v28
	v_cvt_pk_fp8_f32 v2, v7, v3
	v_med3_f32 v4, v4, s85, v252
	v_med3_f32 v6, v6, s85, v252
	v_cvt_pk_fp8_f32 v37, v4, v6 op_sel:[0,0,1]
	v_mul_f32_e32 v4, 0x43800000, v117
	v_mul_f32_e32 v6, 0x43800000, v121
	v_med3_f32 v4, v4, s85, v252
	v_med3_f32 v6, v6, s85, v252
	v_cvt_pk_fp8_f32 v2, v4, v6 op_sel:[0,0,1]
	v_mul_f32_e32 v3, 0x43800000, v57
	v_mul_f32_e32 v4, 0x43800000, v65
	v_med3_f32 v8, v3, s85, v252
	v_med3_f32 v4, v4, s85, v252
	v_mov_b32_e32 v3, v155
	v_cvt_pk_fp8_f32 v3, v8, v4
	v_mul_f32_e32 v6, 0x43800000, v85
	v_mul_f32_e32 v7, 0x43800000, v93
	v_med3_f32 v6, v6, s85, v252
	v_med3_f32 v7, v7, s85, v252
	v_cvt_pk_fp8_f32 v3, v6, v7 op_sel:[0,0,1]
	v_mul_f32_e32 v4, 0x43800000, v25
	v_mul_f32_e32 v6, 0x43800000, v33
	v_med3_f32 v14, v4, s85, v252
	v_med3_f32 v6, v6, s85, v252
	v_mov_b32_e32 v4, v155
	v_cvt_pk_fp8_f32 v4, v14, v6
	v_mul_f32_e32 v5, 0x43800000, v5
	v_mul_f32_e32 v6, 0x43800000, v9
	v_med3_f32 v9, v5, s85, v252
	v_med3_f32 v6, v6, s85, v252
	v_mov_b32_e32 v5, v155
	v_mul_f32_e32 v7, 0x43800000, v49
	v_mul_f32_e32 v8, 0x43800000, v61
	v_cvt_pk_fp8_f32 v5, v9, v6
	v_med3_f32 v7, v7, s85, v252
	v_med3_f32 v8, v8, s85, v252
	v_cvt_pk_fp8_f32 v4, v7, v8 op_sel:[0,0,1]
	v_mul_f32_e32 v7, 0x43800000, v17
	v_mul_f32_e32 v8, 0x43800000, v29
	v_med3_f32 v7, v7, s85, v252
	v_med3_f32 v8, v8, s85, v252
	v_cvt_pk_fp8_f32 v5, v7, v8 op_sel:[0,0,1]
	ds_write_b128 v164, v[34:37] offset:544
	ds_write_b128 v164, v[2:5] offset:816
	s_waitcnt lgkmcnt(0)
	s_barrier
	v_add_co_u32_e32 v2, vcc, s84, v162
	s_mov_b32 s0, 0x802000
	s_nop 0
	v_addc_co_u32_e32 v3, vcc, 0, v163, vcc
	v_add_co_u32_e32 v4, vcc, s0, v162
	s_mov_b32 s0, 0x806000
	s_nop 0
	v_addc_co_u32_e32 v5, vcc, 0, v163, vcc
	global_load_dwordx4 v[90:93], v[2:3], off sc0 nt
	global_load_dwordx4 v[114:117], v[4:5], off sc0 nt
	v_add_co_u32_e32 v2, vcc, s54, v162
	s_nop 1
	v_addc_co_u32_e32 v3, vcc, 0, v163, vcc
	v_add_co_u32_e32 v4, vcc, s0, v162
	s_mov_b32 s0, 0x80a000
	s_nop 0
	v_addc_co_u32_e32 v5, vcc, 0, v163, vcc
	global_load_dwordx4 v[118:121], v[2:3], off sc0 nt
	global_load_dwordx4 v[134:137], v[4:5], off sc0 nt
	v_add_co_u32_e32 v2, vcc, s55, v162
	s_nop 1
	v_addc_co_u32_e32 v3, vcc, 0, v163, vcc
	v_add_co_u32_e32 v4, vcc, s0, v162
	s_mov_b32 s0, 0x80e000
	s_nop 0
	v_addc_co_u32_e32 v5, vcc, 0, v163, vcc
	global_load_dwordx4 v[58:61], v[2:3], off sc0 nt
	global_load_dwordx4 v[70:73], v[4:5], off sc0 nt
	v_add_co_u32_e32 v2, vcc, s64, v162
	s_nop 1
	v_addc_co_u32_e32 v3, vcc, 0, v163, vcc
	v_add_co_u32_e32 v4, vcc, s0, v162
	s_mov_b32 s0, 0x812000
	s_nop 0
	v_addc_co_u32_e32 v5, vcc, 0, v163, vcc
	global_load_dwordx4 v[86:89], v[2:3], off sc0 nt
	global_load_dwordx4 v[94:97], v[4:5], off sc0 nt
	v_add_co_u32_e32 v2, vcc, s65, v162
	s_nop 1
	v_addc_co_u32_e32 v3, vcc, 0, v163, vcc
	v_add_co_u32_e32 v4, vcc, s0, v162
	s_mov_b32 s0, 0x816000
	s_nop 0
	v_addc_co_u32_e32 v5, vcc, 0, v163, vcc
	global_load_dwordx4 v[26:29], v[2:3], off sc0 nt
	global_load_dwordx4 v[34:37], v[4:5], off sc0 nt
	v_add_co_u32_e32 v2, vcc, s68, v162
	s_nop 1
	v_addc_co_u32_e32 v3, vcc, 0, v163, vcc
	v_add_co_u32_e32 v4, vcc, s0, v162
	s_mov_b32 s0, 0x81a000
	s_nop 0
	v_addc_co_u32_e32 v5, vcc, 0, v163, vcc
	global_load_dwordx4 v[54:57], v[2:3], off sc0 nt
	global_load_dwordx4 v[62:65], v[4:5], off sc0 nt
	v_add_co_u32_e32 v2, vcc, s69, v162
	s_nop 1
	v_addc_co_u32_e32 v3, vcc, 0, v163, vcc
	v_add_co_u32_e32 v6, vcc, s0, v162
	s_mov_b32 s0, 0x81e000
	s_nop 0
	v_addc_co_u32_e32 v7, vcc, 0, v163, vcc
	v_add_co_u32_e32 v14, vcc, s70, v162
	global_load_dwordx4 v[2:5], v[2:3], off sc0 nt
	s_nop 0
	global_load_dwordx4 v[6:9], v[6:7], off sc0 nt
	v_addc_co_u32_e32 v15, vcc, 0, v163, vcc
	v_add_co_u32_e32 v16, vcc, s0, v162
	s_nop 1
	v_addc_co_u32_e32 v17, vcc, 0, v163, vcc
	global_load_dwordx4 v[22:25], v[14:15], off sc0 nt
	global_load_dwordx4 v[30:33], v[16:17], off sc0 nt
	ds_read_b128 v[14:17], v142
	s_waitcnt lgkmcnt(0)
	global_store_dwordx4 v[144:145], v[14:17], off offset:512 nt
	ds_read_b128 v[14:17], v146
	s_waitcnt lgkmcnt(0)
	global_store_dwordx4 v[148:149], v[14:17], off offset:512 nt
	ds_read_b128 v[14:17], v150
	s_waitcnt lgkmcnt(0)
	global_store_dwordx4 v[152:153], v[14:17], off offset:512 nt
	ds_read_b128 v[14:17], v158
	s_waitcnt lgkmcnt(0)
	global_store_dwordx4 v[160:161], v[14:17], off offset:512 nt
	s_waitcnt vmcnt(39)
	s_nop 0
	v_mul_f32_e32 v14, 0x43800000, v106
	s_waitcnt vmcnt(38)
	v_mul_f32_e32 v15, 0x43800000, v122
	v_med3_f32 v46, v14, s85, v252
	v_med3_f32 v15, v15, s85, v252
	v_mov_b32_e32 v14, v155
	v_cvt_pk_fp8_f32 v14, v46, v15
	s_waitcnt vmcnt(37)
	v_mul_f32_e32 v16, 0x43800000, v130
	s_waitcnt vmcnt(36)
	v_mul_f32_e32 v17, 0x43800000, v138
	v_med3_f32 v16, v16, s85, v252
	v_med3_f32 v17, v17, s85, v252
	v_cvt_pk_fp8_f32 v14, v16, v17 op_sel:[0,0,1]
	s_waitcnt vmcnt(35)
	v_mul_f32_e32 v15, 0x43800000, v74
	s_waitcnt vmcnt(34)
	v_mul_f32_e32 v16, 0x43800000, v98
	v_med3_f32 v47, v15, s85, v252
	v_med3_f32 v16, v16, s85, v252
	v_mov_b32_e32 v15, v155
	v_cvt_pk_fp8_f32 v15, v47, v16
	s_waitcnt vmcnt(33)
	v_mul_f32_e32 v17, 0x43800000, v110
	s_waitcnt vmcnt(32)
	v_mul_f32_e32 v46, 0x43800000, v126
	v_med3_f32 v17, v17, s85, v252
	v_med3_f32 v46, v46, s85, v252
	v_cvt_pk_fp8_f32 v15, v17, v46 op_sel:[0,0,1]
	s_waitcnt vmcnt(31)
	v_mul_f32_e32 v16, 0x43800000, v38
	s_waitcnt vmcnt(30)
	v_mul_f32_e32 v17, 0x43800000, v50
	v_med3_f32 v47, v16, s85, v252
	v_med3_f32 v17, v17, s85, v252
	v_mov_b32_e32 v16, v155
	v_cvt_pk_fp8_f32 v16, v47, v17
	s_waitcnt vmcnt(27)
	v_mul_f32_e32 v10, 0x43800000, v10
	s_waitcnt vmcnt(26)
	v_mul_f32_e32 v17, 0x43800000, v18
	s_waitcnt vmcnt(25)
	v_mul_f32_e32 v18, 0x43800000, v42
	v_med3_f32 v10, v10, s85, v252
	v_med3_f32 v42, v17, s85, v252
	v_mov_b32_e32 v17, v155
	v_mul_f32_e32 v38, 0x43800000, v78
	v_mul_f32_e32 v46, 0x43800000, v102
	v_cvt_pk_fp8_f32 v17, v10, v42
	v_med3_f32 v38, v38, s85, v252
	v_med3_f32 v46, v46, s85, v252
	v_cvt_pk_fp8_f32 v16, v38, v46 op_sel:[0,0,1]
	s_waitcnt vmcnt(24)
	v_mul_f32_e32 v38, 0x43800000, v66
	v_med3_f32 v18, v18, s85, v252
	v_med3_f32 v38, v38, s85, v252
	v_cvt_pk_fp8_f32 v17, v18, v38 op_sel:[0,0,1]
	v_mul_f32_e32 v10, 0x43800000, v107
	v_med3_f32 v10, v10, s85, v252
	v_mul_f32_e32 v13, 0x43800000, v13
	ds_write_b128 v164, v[14:17] offset:34816
	v_mul_f32_e32 v14, 0x43800000, v123
	v_med3_f32 v17, v14, s85, v252
	v_mov_b32_e32 v14, v155
	v_cvt_pk_fp8_f32 v14, v10, v17
	v_mul_f32_e32 v15, 0x43800000, v131
	v_mul_f32_e32 v16, 0x43800000, v139
	v_med3_f32 v15, v15, s85, v252
	v_med3_f32 v16, v16, s85, v252
	v_cvt_pk_fp8_f32 v14, v15, v16 op_sel:[0,0,1]
	v_mul_f32_e32 v10, 0x43800000, v75
	v_mul_f32_e32 v15, 0x43800000, v99
	v_med3_f32 v10, v10, s85, v252
	v_med3_f32 v18, v15, s85, v252
	v_mov_b32_e32 v15, v155
	v_cvt_pk_fp8_f32 v15, v10, v18
	v_mul_f32_e32 v16, 0x43800000, v111
	v_mul_f32_e32 v17, 0x43800000, v127
	v_med3_f32 v16, v16, s85, v252
	v_med3_f32 v17, v17, s85, v252
	v_cvt_pk_fp8_f32 v15, v16, v17 op_sel:[0,0,1]
	v_mul_f32_e32 v10, 0x43800000, v39
	v_mul_f32_e32 v16, 0x43800000, v51
	v_med3_f32 v10, v10, s85, v252
	v_med3_f32 v38, v16, s85, v252
	v_mov_b32_e32 v16, v155
	v_cvt_pk_fp8_f32 v16, v10, v38
	v_mul_f32_e32 v17, 0x43800000, v79
	v_mul_f32_e32 v18, 0x43800000, v103
	v_med3_f32 v17, v17, s85, v252
	v_med3_f32 v18, v18, s85, v252
	v_cvt_pk_fp8_f32 v16, v17, v18 op_sel:[0,0,1]
	v_mul_f32_e32 v10, 0x43800000, v11
	v_mul_f32_e32 v11, 0x43800000, v19
	v_mul_f32_e32 v17, 0x43800000, v43
	v_med3_f32 v10, v10, s85, v252
	v_med3_f32 v11, v11, s85, v252
	v_med3_f32 v19, v17, s85, v252
	v_mov_b32_e32 v17, v155
	v_cvt_pk_fp8_f32 v17, v10, v11
	v_mul_f32_e32 v18, 0x43800000, v67
	v_med3_f32 v18, v18, s85, v252
	v_mul_f32_e32 v10, 0x43800000, v108
	v_cvt_pk_fp8_f32 v17, v19, v18 op_sel:[0,0,1]
	v_mul_f32_e32 v11, 0x43800000, v124
	v_med3_f32 v10, v10, s85, v252
	v_med3_f32 v11, v11, s85, v252
	ds_write_b128 v164, v[14:17] offset:35088
	v_mul_f32_e32 v14, 0x43800000, v132
	v_med3_f32 v16, v14, s85, v252
	v_mov_b32_e32 v14, v155
	v_cvt_pk_fp8_f32 v14, v10, v11
	v_mul_f32_e32 v15, 0x43800000, v140
	v_med3_f32 v15, v15, s85, v252
	v_mul_f32_e32 v10, 0x43800000, v76
	v_cvt_pk_fp8_f32 v14, v16, v15 op_sel:[0,0,1]
	v_mul_f32_e32 v11, 0x43800000, v100
	v_mul_f32_e32 v15, 0x43800000, v112
	v_med3_f32 v10, v10, s85, v252
	v_med3_f32 v11, v11, s85, v252
	v_med3_f32 v17, v15, s85, v252
	v_mov_b32_e32 v15, v155
	v_cvt_pk_fp8_f32 v15, v10, v11
	v_mul_f32_e32 v16, 0x43800000, v128
	v_med3_f32 v16, v16, s85, v252
	v_mul_f32_e32 v10, 0x43800000, v40
	v_cvt_pk_fp8_f32 v15, v17, v16 op_sel:[0,0,1]
	v_mul_f32_e32 v11, 0x43800000, v52
	v_mul_f32_e32 v16, 0x43800000, v80
	v_med3_f32 v10, v10, s85, v252
	v_med3_f32 v11, v11, s85, v252
	v_med3_f32 v18, v16, s85, v252
	v_mov_b32_e32 v16, v155
	v_cvt_pk_fp8_f32 v16, v10, v11
	v_mul_f32_e32 v17, 0x43800000, v104
	v_med3_f32 v17, v17, s85, v252
	v_mul_f32_e32 v10, 0x43800000, v12
	v_cvt_pk_fp8_f32 v16, v18, v17 op_sel:[0,0,1]
	v_mul_f32_e32 v11, 0x43800000, v20
	v_mul_f32_e32 v17, 0x43800000, v68
	v_med3_f32 v10, v10, s85, v252
	v_med3_f32 v11, v11, s85, v252
	v_med3_f32 v18, v17, s85, v252
	v_mov_b32_e32 v17, v155
	v_cvt_pk_fp8_f32 v17, v10, v11
	v_mul_f32_e32 v12, 0x43800000, v44
	v_med3_f32 v12, v12, s85, v252
	v_mul_f32_e32 v10, 0x43800000, v109
	v_cvt_pk_fp8_f32 v17, v12, v18 op_sel:[0,0,1]
	v_mul_f32_e32 v11, 0x43800000, v125
	v_med3_f32 v11, v11, s85, v252
	v_mul_f32_e32 v12, 0x43800000, v133
	ds_write_b128 v164, v[14:17] offset:35360
	v_med3_f32 v15, v10, s85, v252
	v_mov_b32_e32 v10, v155
	v_cvt_pk_fp8_f32 v10, v15, v11
	v_mul_f32_e32 v14, 0x43800000, v141
	v_med3_f32 v12, v12, s85, v252
	v_med3_f32 v14, v14, s85, v252
	v_cvt_pk_fp8_f32 v10, v12, v14 op_sel:[0,0,1]
	v_mul_f32_e32 v11, 0x43800000, v77
	v_mul_f32_e32 v12, 0x43800000, v101
	v_med3_f32 v16, v11, s85, v252
	v_med3_f32 v12, v12, s85, v252
	v_mov_b32_e32 v11, v155
	v_cvt_pk_fp8_f32 v11, v16, v12
	v_mul_f32_e32 v14, 0x43800000, v113
	v_mul_f32_e32 v15, 0x43800000, v129
	v_med3_f32 v14, v14, s85, v252
	v_med3_f32 v15, v15, s85, v252
	v_cvt_pk_fp8_f32 v11, v14, v15 op_sel:[0,0,1]
	v_mul_f32_e32 v12, 0x43800000, v41
	v_mul_f32_e32 v14, 0x43800000, v53
	v_med3_f32 v17, v12, s85, v252
	v_med3_f32 v14, v14, s85, v252
	v_mov_b32_e32 v12, v155
	v_cvt_pk_fp8_f32 v12, v17, v14
	v_mul_f32_e32 v14, 0x43800000, v21
	v_med3_f32 v17, v13, s85, v252
	v_med3_f32 v14, v14, s85, v252
	v_mov_b32_e32 v13, v155
	v_mul_f32_e32 v15, 0x43800000, v81
	v_mul_f32_e32 v16, 0x43800000, v105
	v_cvt_pk_fp8_f32 v13, v17, v14
	v_med3_f32 v15, v15, s85, v252
	v_med3_f32 v16, v16, s85, v252
	v_cvt_pk_fp8_f32 v12, v15, v16 op_sel:[0,0,1]
	v_mul_f32_e32 v15, 0x43800000, v45
	v_mul_f32_e32 v16, 0x43800000, v69
	v_med3_f32 v15, v15, s85, v252
	v_med3_f32 v16, v16, s85, v252
	v_cvt_pk_fp8_f32 v13, v15, v16 op_sel:[0,0,1]
	ds_write_b128 v164, v[10:13] offset:35632
	s_waitcnt lgkmcnt(0)
	s_barrier
	s_mov_b32 s0, 0xa00000
	v_add_co_u32_e32 v10, vcc, s0, v162
	s_mov_b32 s0, 0xa02000
	s_nop 0
	v_addc_co_u32_e32 v11, vcc, 0, v163, vcc
	v_add_co_u32_e32 v12, vcc, s0, v162
	s_mov_b32 s0, 0xa04000
	s_nop 0
	v_addc_co_u32_e32 v13, vcc, 0, v163, vcc
	global_load_dwordx4 v[98:101], v[10:11], off sc0 nt
	global_load_dwordx4 v[106:109], v[12:13], off sc0 nt
	v_add_co_u32_e32 v10, vcc, s0, v162
	s_mov_b32 s0, 0xa06000
	s_nop 0
	v_addc_co_u32_e32 v11, vcc, 0, v163, vcc
	v_add_co_u32_e32 v12, vcc, s0, v162
	s_mov_b32 s0, 0xa08000
	s_nop 0
	v_addc_co_u32_e32 v13, vcc, 0, v163, vcc
	global_load_dwordx4 v[122:125], v[10:11], off sc0 nt
	global_load_dwordx4 v[126:129], v[12:13], off sc0 nt
	v_add_co_u32_e32 v10, vcc, s0, v162
	s_mov_b32 s0, 0xa0a000
	s_nop 0
	v_addc_co_u32_e32 v11, vcc, 0, v163, vcc
	v_add_co_u32_e32 v12, vcc, s0, v162
	s_mov_b32 s0, 0xa0c000
	s_nop 0
	v_addc_co_u32_e32 v13, vcc, 0, v163, vcc
	global_load_dwordx4 v[66:69], v[10:11], off sc0 nt
	global_load_dwordx4 v[78:81], v[12:13], off sc0 nt
	v_add_co_u32_e32 v10, vcc, s0, v162
	s_mov_b32 s0, 0xa0e000
	s_nop 0
	v_addc_co_u32_e32 v11, vcc, 0, v163, vcc
	v_add_co_u32_e32 v12, vcc, s0, v162
	s_mov_b32 s0, 0xa10000
	s_nop 0
	v_addc_co_u32_e32 v13, vcc, 0, v163, vcc
	global_load_dwordx4 v[102:105], v[10:11], off sc0 nt
	global_load_dwordx4 v[110:113], v[12:13], off sc0 nt
	v_add_co_u32_e32 v10, vcc, s0, v162
	s_mov_b32 s0, 0xa12000
	s_nop 0
	v_addc_co_u32_e32 v11, vcc, 0, v163, vcc
	v_add_co_u32_e32 v12, vcc, s0, v162
	s_mov_b32 s0, 0xa14000
	s_nop 0
	v_addc_co_u32_e32 v13, vcc, 0, v163, vcc
	global_load_dwordx4 v[38:41], v[10:11], off sc0 nt
	global_load_dwordx4 v[46:49], v[12:13], off sc0 nt
	v_add_co_u32_e32 v10, vcc, s0, v162
	s_mov_b32 s0, 0xa16000
	s_nop 0
	v_addc_co_u32_e32 v11, vcc, 0, v163, vcc
	v_add_co_u32_e32 v12, vcc, s0, v162
	s_mov_b32 s0, 0xa18000
	s_nop 0
	v_addc_co_u32_e32 v13, vcc, 0, v163, vcc
	global_load_dwordx4 v[74:77], v[10:11], off sc0 nt
	global_load_dwordx4 v[82:85], v[12:13], off sc0 nt
	v_add_co_u32_e32 v10, vcc, s0, v162
	s_mov_b32 s0, 0xa1a000
	s_nop 0
	v_addc_co_u32_e32 v11, vcc, 0, v163, vcc
	v_add_co_u32_e32 v14, vcc, s0, v162
	s_mov_b32 s0, 0xa1c000
	s_nop 0
	v_addc_co_u32_e32 v15, vcc, 0, v163, vcc
	v_add_co_u32_e32 v18, vcc, s0, v162
	s_mov_b32 s0, 0xa1e000
	s_nop 0
	v_addc_co_u32_e32 v19, vcc, 0, v163, vcc
	v_add_co_u32_e32 v20, vcc, s0, v162
	global_load_dwordx4 v[10:13], v[10:11], off sc0 nt
	s_nop 0
	global_load_dwordx4 v[14:17], v[14:15], off sc0 nt
	v_addc_co_u32_e32 v21, vcc, 0, v163, vcc
	global_load_dwordx4 v[42:45], v[18:19], off sc0 nt
	global_load_dwordx4 v[50:53], v[20:21], off sc0 nt
	ds_read_b128 v[18:21], v142 offset:34816
	s_waitcnt lgkmcnt(0)
	global_store_dwordx4 v[144:145], v[18:21], off offset:768 nt
	ds_read_b128 v[18:21], v146 offset:34816
	s_waitcnt lgkmcnt(0)
	global_store_dwordx4 v[148:149], v[18:21], off offset:768 nt
	ds_read_b128 v[18:21], v150 offset:34816
	s_waitcnt lgkmcnt(0)
	global_store_dwordx4 v[152:153], v[18:21], off offset:768 nt
	ds_read_b128 v[18:21], v158 offset:34816
	s_waitcnt lgkmcnt(0)
	global_store_dwordx4 v[160:161], v[18:21], off offset:768 nt
	s_waitcnt vmcnt(39)
	s_nop 0
	v_mul_f32_e32 v18, 0x43800000, v90
	s_waitcnt vmcnt(38)
	v_mul_f32_e32 v19, 0x43800000, v114
	v_med3_f32 v90, v18, s85, v252
	v_med3_f32 v19, v19, s85, v252
	v_mov_b32_e32 v18, v155
	v_cvt_pk_fp8_f32 v18, v90, v19
	s_waitcnt vmcnt(37)
	v_mul_f32_e32 v20, 0x43800000, v118
	s_waitcnt vmcnt(36)
	v_mul_f32_e32 v21, 0x43800000, v134
	v_med3_f32 v20, v20, s85, v252
	v_med3_f32 v21, v21, s85, v252
	v_cvt_pk_fp8_f32 v18, v20, v21 op_sel:[0,0,1]
	s_waitcnt vmcnt(35)
	v_mul_f32_e32 v19, 0x43800000, v58
	s_waitcnt vmcnt(34)
	v_mul_f32_e32 v20, 0x43800000, v70
	v_med3_f32 v70, v19, s85, v252
	v_med3_f32 v20, v20, s85, v252
	v_mov_b32_e32 v19, v155
	v_cvt_pk_fp8_f32 v19, v70, v20
	s_waitcnt vmcnt(33)
	v_mul_f32_e32 v21, 0x43800000, v86
	s_waitcnt vmcnt(32)
	v_mul_f32_e32 v58, 0x43800000, v94
	v_med3_f32 v21, v21, s85, v252
	v_med3_f32 v58, v58, s85, v252
	v_cvt_pk_fp8_f32 v19, v21, v58 op_sel:[0,0,1]
	s_waitcnt vmcnt(31)
	v_mul_f32_e32 v20, 0x43800000, v26
	s_waitcnt vmcnt(30)
	v_mul_f32_e32 v21, 0x43800000, v34
	s_waitcnt vmcnt(29)
	v_mul_f32_e32 v26, 0x43800000, v54
	v_med3_f32 v54, v20, s85, v252
	v_med3_f32 v21, v21, s85, v252
	v_mov_b32_e32 v20, v155
	v_cvt_pk_fp8_f32 v20, v54, v21
	s_waitcnt vmcnt(28)
	v_mul_f32_e32 v34, 0x43800000, v62
	v_med3_f32 v26, v26, s85, v252
	v_med3_f32 v34, v34, s85, v252
	s_waitcnt vmcnt(27)
	v_mul_f32_e32 v2, 0x43800000, v2
	s_waitcnt vmcnt(26)
	v_mul_f32_e32 v6, 0x43800000, v6
	s_waitcnt vmcnt(25)
	v_mul_f32_e32 v21, 0x43800000, v22
	v_cvt_pk_fp8_f32 v20, v26, v34 op_sel:[0,0,1]
	v_med3_f32 v2, v2, s85, v252
	v_med3_f32 v6, v6, s85, v252
	v_med3_f32 v26, v21, s85, v252
	v_mov_b32_e32 v21, v155
	v_cvt_pk_fp8_f32 v21, v2, v6
	s_waitcnt vmcnt(24)
	v_mul_f32_e32 v22, 0x43800000, v30
	v_med3_f32 v22, v22, s85, v252
	v_mul_f32_e32 v2, 0x43800000, v91
	v_cvt_pk_fp8_f32 v21, v26, v22 op_sel:[0,0,1]
	v_mul_f32_e32 v6, 0x43800000, v115
	v_med3_f32 v2, v2, s85, v252
	v_med3_f32 v6, v6, s85, v252
	ds_write_b128 v164, v[18:21]
	v_mul_f32_e32 v18, 0x43800000, v119
	v_med3_f32 v20, v18, s85, v252
	v_mov_b32_e32 v18, v155
	v_cvt_pk_fp8_f32 v18, v2, v6
	v_mul_f32_e32 v19, 0x43800000, v135
	v_med3_f32 v19, v19, s85, v252
	v_mul_f32_e32 v2, 0x43800000, v59
	v_cvt_pk_fp8_f32 v18, v20, v19 op_sel:[0,0,1]
	v_mul_f32_e32 v6, 0x43800000, v71
	v_mul_f32_e32 v19, 0x43800000, v87
	v_med3_f32 v2, v2, s85, v252
	v_med3_f32 v6, v6, s85, v252
	v_med3_f32 v21, v19, s85, v252
	v_mov_b32_e32 v19, v155
	v_cvt_pk_fp8_f32 v19, v2, v6
	v_mul_f32_e32 v20, 0x43800000, v95
	v_med3_f32 v20, v20, s85, v252
	v_mul_f32_e32 v2, 0x43800000, v27
	v_cvt_pk_fp8_f32 v19, v21, v20 op_sel:[0,0,1]
	v_mul_f32_e32 v6, 0x43800000, v35
	v_mul_f32_e32 v20, 0x43800000, v55
	v_med3_f32 v2, v2, s85, v252
	v_med3_f32 v6, v6, s85, v252
	v_med3_f32 v22, v20, s85, v252
	v_mov_b32_e32 v20, v155
	v_cvt_pk_fp8_f32 v20, v2, v6
	v_mul_f32_e32 v21, 0x43800000, v63
	v_med3_f32 v21, v21, s85, v252
	v_mul_f32_e32 v2, 0x43800000, v3
	v_mul_f32_e32 v3, 0x43800000, v7
	v_cvt_pk_fp8_f32 v20, v22, v21 op_sel:[0,0,1]
	v_med3_f32 v2, v2, s85, v252
	v_med3_f32 v3, v3, s85, v252
	v_mov_b32_e32 v21, v155
	v_cvt_pk_fp8_f32 v21, v2, v3
	v_mul_f32_e32 v6, 0x43800000, v23
	v_mul_f32_e32 v7, 0x43800000, v31
	v_med3_f32 v6, v6, s85, v252
	v_med3_f32 v7, v7, s85, v252
	v_cvt_pk_fp8_f32 v21, v6, v7 op_sel:[0,0,1]
	v_mul_f32_e32 v2, 0x43800000, v92
	v_mul_f32_e32 v3, 0x43800000, v116
	v_med3_f32 v2, v2, s85, v252
	ds_write_b128 v164, v[18:21] offset:272
	v_med3_f32 v3, v3, s85, v252
	v_mov_b32_e32 v18, v155
	v_cvt_pk_fp8_f32 v18, v2, v3
	v_mul_f32_e32 v2, 0x43800000, v60
	v_mul_f32_e32 v3, 0x43800000, v72
	v_med3_f32 v2, v2, s85, v252
	v_med3_f32 v3, v3, s85, v252
	v_mov_b32_e32 v19, v155
	v_mul_f32_e32 v6, 0x43800000, v120
	v_mul_f32_e32 v7, 0x43800000, v136
	v_cvt_pk_fp8_f32 v19, v2, v3
	v_mul_f32_e32 v2, 0x43800000, v28
	v_mul_f32_e32 v3, 0x43800000, v36
	v_med3_f32 v6, v6, s85, v252
	v_med3_f32 v7, v7, s85, v252
	v_med3_f32 v2, v2, s85, v252
	v_med3_f32 v3, v3, s85, v252
	v_mov_b32_e32 v20, v155
	v_cvt_pk_fp8_f32 v18, v6, v7 op_sel:[0,0,1]
	v_mul_f32_e32 v6, 0x43800000, v88
	v_mul_f32_e32 v7, 0x43800000, v96
	v_cvt_pk_fp8_f32 v20, v2, v3
	v_med3_f32 v6, v6, s85, v252
	v_med3_f32 v7, v7, s85, v252
	v_mul_f32_e32 v2, 0x43800000, v4
	v_mul_f32_e32 v3, 0x43800000, v8
	v_cvt_pk_fp8_f32 v19, v6, v7 op_sel:[0,0,1]
	v_mul_f32_e32 v6, 0x43800000, v56
	v_mul_f32_e32 v7, 0x43800000, v64
	v_med3_f32 v2, v2, s85, v252
	v_med3_f32 v3, v3, s85, v252
	v_mov_b32_e32 v21, v155
	v_med3_f32 v6, v6, s85, v252
	v_med3_f32 v7, v7, s85, v252
	v_cvt_pk_fp8_f32 v21, v2, v3
	v_mul_f32_e32 v2, 0x43800000, v93
	v_mul_f32_e32 v3, 0x43800000, v117
	v_cvt_pk_fp8_f32 v20, v6, v7 op_sel:[0,0,1]
	v_med3_f32 v7, v2, s85, v252
	v_med3_f32 v3, v3, s85, v252
	v_mov_b32_e32 v2, v155
	v_mul_f32_e32 v4, 0x43800000, v24
	v_mul_f32_e32 v6, 0x43800000, v32
	v_cvt_pk_fp8_f32 v2, v7, v3
	v_med3_f32 v4, v4, s85, v252
	v_med3_f32 v6, v6, s85, v252
	v_cvt_pk_fp8_f32 v21, v4, v6 op_sel:[0,0,1]
	v_mul_f32_e32 v4, 0x43800000, v121
	v_mul_f32_e32 v6, 0x43800000, v137
	v_med3_f32 v4, v4, s85, v252
	v_med3_f32 v6, v6, s85, v252
	v_cvt_pk_fp8_f32 v2, v4, v6 op_sel:[0,0,1]
	v_mul_f32_e32 v3, 0x43800000, v61
	v_mul_f32_e32 v4, 0x43800000, v73
	v_med3_f32 v8, v3, s85, v252
	v_med3_f32 v4, v4, s85, v252
	v_mov_b32_e32 v3, v155
	v_cvt_pk_fp8_f32 v3, v8, v4
	v_mul_f32_e32 v6, 0x43800000, v89
	v_mul_f32_e32 v7, 0x43800000, v97
	v_med3_f32 v6, v6, s85, v252
	v_med3_f32 v7, v7, s85, v252
	v_cvt_pk_fp8_f32 v3, v6, v7 op_sel:[0,0,1]
	v_mul_f32_e32 v4, 0x43800000, v29
	v_mul_f32_e32 v6, 0x43800000, v37
	ds_write_b128 v164, v[18:21] offset:544
	v_med3_f32 v18, v4, s85, v252
	v_med3_f32 v6, v6, s85, v252
	v_mov_b32_e32 v4, v155
	v_cvt_pk_fp8_f32 v4, v18, v6
	v_mul_f32_e32 v5, 0x43800000, v5
	v_mul_f32_e32 v6, 0x43800000, v9
	v_med3_f32 v9, v5, s85, v252
	v_med3_f32 v6, v6, s85, v252
	v_mov_b32_e32 v5, v155
	v_mul_f32_e32 v7, 0x43800000, v57
	v_mul_f32_e32 v8, 0x43800000, v65
	v_cvt_pk_fp8_f32 v5, v9, v6
	v_med3_f32 v7, v7, s85, v252
	v_med3_f32 v8, v8, s85, v252
	v_cvt_pk_fp8_f32 v4, v7, v8 op_sel:[0,0,1]
	v_mul_f32_e32 v7, 0x43800000, v25
	v_mul_f32_e32 v8, 0x43800000, v33
	v_med3_f32 v7, v7, s85, v252
	v_med3_f32 v8, v8, s85, v252
	v_cvt_pk_fp8_f32 v5, v7, v8 op_sel:[0,0,1]
	ds_write_b128 v164, v[2:5] offset:816
	s_waitcnt lgkmcnt(0)
	s_barrier
	v_add_co_u32_e32 v2, vcc, s73, v162
	s_mov_b32 s0, 0xc02000
	s_nop 0
	v_addc_co_u32_e32 v3, vcc, 0, v163, vcc
	v_add_co_u32_e32 v4, vcc, s0, v162
	s_mov_b32 s0, 0xc06000
	s_nop 0
	v_addc_co_u32_e32 v5, vcc, 0, v163, vcc
	global_load_dwordx4 v[86:89], v[2:3], off sc0 nt
	global_load_dwordx4 v[94:97], v[4:5], off sc0 nt
	v_add_co_u32_e32 v2, vcc, s75, v162
	s_nop 1
	v_addc_co_u32_e32 v3, vcc, 0, v163, vcc
	v_add_co_u32_e32 v4, vcc, s0, v162
	s_mov_b32 s0, 0xc0a000
	s_nop 0
	v_addc_co_u32_e32 v5, vcc, 0, v163, vcc
	global_load_dwordx4 v[114:117], v[2:3], off sc0 nt
	global_load_dwordx4 v[118:121], v[4:5], off sc0 nt
	v_add_co_u32_e32 v2, vcc, s76, v162
	s_nop 1
	v_addc_co_u32_e32 v3, vcc, 0, v163, vcc
	v_add_co_u32_e32 v4, vcc, s0, v162
	s_mov_b32 s0, 0xc0e000
	s_nop 0
	v_addc_co_u32_e32 v5, vcc, 0, v163, vcc
	global_load_dwordx4 v[54:57], v[2:3], off sc0 nt
	global_load_dwordx4 v[62:65], v[4:5], off sc0 nt
	v_add_co_u32_e32 v2, vcc, s82, v162
	s_nop 1
	v_addc_co_u32_e32 v3, vcc, 0, v163, vcc
	v_add_co_u32_e32 v4, vcc, s0, v162
	s_mov_b32 s0, 0xc12000
	s_nop 0
	v_addc_co_u32_e32 v5, vcc, 0, v163, vcc
	global_load_dwordx4 v[70:73], v[2:3], off sc0 nt
	global_load_dwordx4 v[90:93], v[4:5], off sc0 nt
	v_add_co_u32_e32 v2, vcc, s89, v162
	s_nop 1
	v_addc_co_u32_e32 v3, vcc, 0, v163, vcc
	v_add_co_u32_e32 v4, vcc, s0, v162
	s_mov_b32 s0, 0xc16000
	s_nop 0
	v_addc_co_u32_e32 v5, vcc, 0, v163, vcc
	global_load_dwordx4 v[22:25], v[2:3], off sc0 nt
	global_load_dwordx4 v[30:33], v[4:5], off sc0 nt
	v_add_co_u32_e32 v2, vcc, s91, v162
	s_nop 1
	v_addc_co_u32_e32 v3, vcc, 0, v163, vcc
	v_add_co_u32_e32 v4, vcc, s0, v162
	s_mov_b32 s0, 0xc1a000
	s_nop 0
	v_addc_co_u32_e32 v5, vcc, 0, v163, vcc
	global_load_dwordx4 v[34:37], v[2:3], off sc0 nt
	global_load_dwordx4 v[58:61], v[4:5], off sc0 nt
	v_add_co_u32_e32 v2, vcc, s92, v162
	s_nop 1
	v_addc_co_u32_e32 v3, vcc, 0, v163, vcc
	v_add_co_u32_e32 v6, vcc, s0, v162
	s_mov_b32 s0, 0xc1e000
	s_nop 0
	v_addc_co_u32_e32 v7, vcc, 0, v163, vcc
	v_add_co_u32_e32 v18, vcc, s93, v162
	global_load_dwordx4 v[2:5], v[2:3], off sc0 nt
	s_nop 0
	global_load_dwordx4 v[6:9], v[6:7], off sc0 nt
	v_addc_co_u32_e32 v19, vcc, 0, v163, vcc
	v_add_co_u32_e32 v26, vcc, s0, v162
	s_nop 1
	v_addc_co_u32_e32 v27, vcc, 0, v163, vcc
	global_load_dwordx4 v[18:21], v[18:19], off sc0 nt
	s_nop 0
	global_load_dwordx4 v[26:29], v[26:27], off sc0 nt
	ds_read_b128 v[130:133], v142
	s_waitcnt lgkmcnt(0)
	global_store_dwordx4 v[144:145], v[130:133], off offset:1024 nt
	ds_read_b128 v[130:133], v146
	s_waitcnt lgkmcnt(0)
	global_store_dwordx4 v[148:149], v[130:133], off offset:1024 nt
	ds_read_b128 v[130:133], v150
	s_waitcnt lgkmcnt(0)
	global_store_dwordx4 v[152:153], v[130:133], off offset:1024 nt
	ds_read_b128 v[130:133], v158
	s_waitcnt lgkmcnt(0)
	global_store_dwordx4 v[160:161], v[130:133], off offset:1024 nt
	s_waitcnt vmcnt(39)
	v_mul_f32_e32 v98, 0x43800000, v98
	s_waitcnt vmcnt(38)
	v_mul_f32_e32 v106, 0x43800000, v106
	s_waitcnt vmcnt(35)
	v_mul_f32_e32 v66, 0x43800000, v66
	s_waitcnt vmcnt(34)
	v_mul_f32_e32 v78, 0x43800000, v78
	s_waitcnt vmcnt(31)
	v_mul_f32_e32 v38, 0x43800000, v38
	s_waitcnt vmcnt(30)
	v_mul_f32_e32 v46, 0x43800000, v46
	s_waitcnt vmcnt(27)
	v_mul_f32_e32 v10, 0x43800000, v10
	s_waitcnt vmcnt(26)
	v_mul_f32_e32 v14, 0x43800000, v14
	v_med3_f32 v98, v98, s85, v252
	v_med3_f32 v106, v106, s85, v252
	v_mov_b32_e32 v130, v155
	v_med3_f32 v66, v66, s85, v252
	v_med3_f32 v78, v78, s85, v252
	v_mov_b32_e32 v131, v155
	v_med3_f32 v38, v38, s85, v252
	v_med3_f32 v46, v46, s85, v252
	v_mov_b32_e32 v132, v155
	v_med3_f32 v10, v10, s85, v252
	v_med3_f32 v14, v14, s85, v252
	v_mov_b32_e32 v133, v155
	v_cvt_pk_fp8_f32 v130, v98, v106
	v_cvt_pk_fp8_f32 v131, v66, v78
	v_cvt_pk_fp8_f32 v132, v38, v46
	v_cvt_pk_fp8_f32 v133, v10, v14
	v_mul_f32_e32 v122, 0x43800000, v122
	v_mul_f32_e32 v126, 0x43800000, v126
	v_mul_f32_e32 v98, 0x43800000, v102
	v_mul_f32_e32 v102, 0x43800000, v110
	v_mul_f32_e32 v66, 0x43800000, v74
	v_mul_f32_e32 v74, 0x43800000, v82
	s_waitcnt vmcnt(25)
	v_mul_f32_e32 v38, 0x43800000, v42
	s_waitcnt vmcnt(24)
	v_mul_f32_e32 v42, 0x43800000, v50
	v_med3_f32 v122, v122, s85, v252
	v_med3_f32 v126, v126, s85, v252
	v_med3_f32 v98, v98, s85, v252
	v_med3_f32 v102, v102, s85, v252
	v_med3_f32 v66, v66, s85, v252
	v_med3_f32 v74, v74, s85, v252
	v_med3_f32 v38, v38, s85, v252
	v_med3_f32 v42, v42, s85, v252
	v_cvt_pk_fp8_f32 v130, v122, v126 op_sel:[0,0,1]
	v_cvt_pk_fp8_f32 v131, v98, v102 op_sel:[0,0,1]
	v_cvt_pk_fp8_f32 v132, v66, v74 op_sel:[0,0,1]
	v_cvt_pk_fp8_f32 v133, v38, v42 op_sel:[0,0,1]
	v_mul_f32_e32 v10, 0x43800000, v99
	v_mul_f32_e32 v14, 0x43800000, v107
	v_med3_f32 v10, v10, s85, v252
	ds_write_b128 v164, v[130:133] offset:34816
	v_med3_f32 v14, v14, s85, v252
	v_mov_b32_e32 v130, v155
	v_cvt_pk_fp8_f32 v130, v10, v14
	v_mul_f32_e32 v10, 0x43800000, v67
	v_mul_f32_e32 v14, 0x43800000, v79
	v_med3_f32 v10, v10, s85, v252
	v_med3_f32 v14, v14, s85, v252
	v_mov_b32_e32 v131, v155
	v_cvt_pk_fp8_f32 v131, v10, v14
	v_mul_f32_e32 v10, 0x43800000, v39
	v_mul_f32_e32 v14, 0x43800000, v47
	v_med3_f32 v10, v10, s85, v252
	v_med3_f32 v14, v14, s85, v252
	v_mov_b32_e32 v132, v155
	v_mul_f32_e32 v38, 0x43800000, v123
	v_mul_f32_e32 v42, 0x43800000, v127
	v_cvt_pk_fp8_f32 v132, v10, v14
	v_mul_f32_e32 v10, 0x43800000, v11
	v_mul_f32_e32 v11, 0x43800000, v15
	v_med3_f32 v38, v38, s85, v252
	v_med3_f32 v42, v42, s85, v252
	v_med3_f32 v10, v10, s85, v252
	v_med3_f32 v11, v11, s85, v252
	v_mov_b32_e32 v133, v155
	v_cvt_pk_fp8_f32 v130, v38, v42 op_sel:[0,0,1]
	v_mul_f32_e32 v38, 0x43800000, v103
	v_mul_f32_e32 v42, 0x43800000, v111
	v_cvt_pk_fp8_f32 v133, v10, v11
	v_med3_f32 v38, v38, s85, v252
	v_med3_f32 v42, v42, s85, v252
	v_cvt_pk_fp8_f32 v131, v38, v42 op_sel:[0,0,1]
	v_mul_f32_e32 v38, 0x43800000, v75
	v_mul_f32_e32 v39, 0x43800000, v83
	v_mul_f32_e32 v14, 0x43800000, v43
	v_mul_f32_e32 v15, 0x43800000, v51
	v_med3_f32 v38, v38, s85, v252
	v_med3_f32 v39, v39, s85, v252
	v_med3_f32 v14, v14, s85, v252
	v_med3_f32 v15, v15, s85, v252
	v_cvt_pk_fp8_f32 v132, v38, v39 op_sel:[0,0,1]
	v_cvt_pk_fp8_f32 v133, v14, v15 op_sel:[0,0,1]
	v_mul_f32_e32 v10, 0x43800000, v100
	v_mul_f32_e32 v11, 0x43800000, v108
	v_med3_f32 v10, v10, s85, v252
	ds_write_b128 v164, v[130:133] offset:35088
	v_med3_f32 v11, v11, s85, v252
	v_mov_b32_e32 v130, v155
	v_cvt_pk_fp8_f32 v130, v10, v11
	v_mul_f32_e32 v10, 0x43800000, v68
	v_mul_f32_e32 v11, 0x43800000, v80
	v_med3_f32 v10, v10, s85, v252
	v_med3_f32 v11, v11, s85, v252
	v_mov_b32_e32 v131, v155
	v_mul_f32_e32 v14, 0x43800000, v124
	v_mul_f32_e32 v15, 0x43800000, v128
	v_cvt_pk_fp8_f32 v131, v10, v11
	v_mul_f32_e32 v10, 0x43800000, v40
	v_mul_f32_e32 v11, 0x43800000, v48
	v_med3_f32 v14, v14, s85, v252
	v_med3_f32 v15, v15, s85, v252
	v_med3_f32 v10, v10, s85, v252
	v_med3_f32 v11, v11, s85, v252
	v_mov_b32_e32 v132, v155
	v_cvt_pk_fp8_f32 v130, v14, v15 op_sel:[0,0,1]
	v_mul_f32_e32 v14, 0x43800000, v104
	v_mul_f32_e32 v15, 0x43800000, v112
	v_cvt_pk_fp8_f32 v132, v10, v11
	v_med3_f32 v14, v14, s85, v252
	v_med3_f32 v15, v15, s85, v252
	v_mul_f32_e32 v10, 0x43800000, v12
	v_mul_f32_e32 v11, 0x43800000, v16
	v_cvt_pk_fp8_f32 v131, v14, v15 op_sel:[0,0,1]
	v_mul_f32_e32 v14, 0x43800000, v76
	v_mul_f32_e32 v15, 0x43800000, v84
	v_med3_f32 v10, v10, s85, v252
	v_med3_f32 v11, v11, s85, v252
	v_mov_b32_e32 v133, v155
	v_med3_f32 v14, v14, s85, v252
	v_med3_f32 v15, v15, s85, v252
	v_cvt_pk_fp8_f32 v133, v10, v11
	v_mul_f32_e32 v10, 0x43800000, v101
	v_mul_f32_e32 v11, 0x43800000, v109
	v_cvt_pk_fp8_f32 v132, v14, v15 op_sel:[0,0,1]
	v_med3_f32 v15, v10, s85, v252
	v_med3_f32 v11, v11, s85, v252
	v_mov_b32_e32 v10, v155
	v_mul_f32_e32 v12, 0x43800000, v44
	v_mul_f32_e32 v14, 0x43800000, v52
	v_cvt_pk_fp8_f32 v10, v15, v11
	v_med3_f32 v12, v12, s85, v252
	v_med3_f32 v14, v14, s85, v252
	v_cvt_pk_fp8_f32 v133, v12, v14 op_sel:[0,0,1]
	v_mul_f32_e32 v12, 0x43800000, v125
	v_mul_f32_e32 v14, 0x43800000, v129
	v_med3_f32 v12, v12, s85, v252
	v_med3_f32 v14, v14, s85, v252
	v_cvt_pk_fp8_f32 v10, v12, v14 op_sel:[0,0,1]
	v_mul_f32_e32 v11, 0x43800000, v69
	v_mul_f32_e32 v12, 0x43800000, v81
	v_med3_f32 v16, v11, s85, v252
	v_med3_f32 v12, v12, s85, v252
	v_mov_b32_e32 v11, v155
	v_cvt_pk_fp8_f32 v11, v16, v12
	v_mul_f32_e32 v14, 0x43800000, v105
	v_mul_f32_e32 v15, 0x43800000, v113
	v_med3_f32 v14, v14, s85, v252
	v_med3_f32 v15, v15, s85, v252
	v_cvt_pk_fp8_f32 v11, v14, v15 op_sel:[0,0,1]
	v_mul_f32_e32 v12, 0x43800000, v41
	v_mul_f32_e32 v14, 0x43800000, v49
	v_med3_f32 v38, v12, s85, v252
	v_med3_f32 v14, v14, s85, v252
	v_mov_b32_e32 v12, v155
	v_cvt_pk_fp8_f32 v12, v38, v14
	v_mul_f32_e32 v13, 0x43800000, v13
	v_mul_f32_e32 v14, 0x43800000, v17
	v_med3_f32 v17, v13, s85, v252
	v_med3_f32 v14, v14, s85, v252
	v_mov_b32_e32 v13, v155
	v_mul_f32_e32 v15, 0x43800000, v77
	v_mul_f32_e32 v16, 0x43800000, v85
	v_cvt_pk_fp8_f32 v13, v17, v14
	v_med3_f32 v15, v15, s85, v252
	v_med3_f32 v16, v16, s85, v252
	v_cvt_pk_fp8_f32 v12, v15, v16 op_sel:[0,0,1]
	v_mul_f32_e32 v15, 0x43800000, v45
	v_mul_f32_e32 v16, 0x43800000, v53
	v_med3_f32 v15, v15, s85, v252
	v_med3_f32 v16, v16, s85, v252
	v_cvt_pk_fp8_f32 v13, v15, v16 op_sel:[0,0,1]
	ds_write_b128 v164, v[130:133] offset:35360
	ds_write_b128 v164, v[10:13] offset:35632
	s_waitcnt lgkmcnt(0)
	s_barrier
	s_mov_b32 s0, 0xe00000
	v_add_co_u32_e32 v10, vcc, s0, v162
	s_mov_b32 s0, 0xe02000
	s_nop 0
	v_addc_co_u32_e32 v11, vcc, 0, v163, vcc
	v_add_co_u32_e32 v12, vcc, s0, v162
	s_mov_b32 s0, 0xe04000
	s_nop 0
	v_addc_co_u32_e32 v13, vcc, 0, v163, vcc
	global_load_dwordx4 v[98:101], v[10:11], off sc0 nt
	global_load_dwordx4 v[106:109], v[12:13], off sc0 nt
	v_add_co_u32_e32 v10, vcc, s0, v162
	s_mov_b32 s0, 0xe06000
	s_nop 0
	v_addc_co_u32_e32 v11, vcc, 0, v163, vcc
	v_add_co_u32_e32 v12, vcc, s0, v162
	s_mov_b32 s0, 0xe08000
	s_nop 0
	v_addc_co_u32_e32 v13, vcc, 0, v163, vcc
	global_load_dwordx4 v[122:125], v[10:11], off sc0 nt
	global_load_dwordx4 v[126:129], v[12:13], off sc0 nt
	v_add_co_u32_e32 v10, vcc, s0, v162
	s_mov_b32 s0, 0xe0a000
	s_nop 0
	v_addc_co_u32_e32 v11, vcc, 0, v163, vcc
	v_add_co_u32_e32 v12, vcc, s0, v162
	s_mov_b32 s0, 0xe0c000
	s_nop 0
	v_addc_co_u32_e32 v13, vcc, 0, v163, vcc
	global_load_dwordx4 v[66:69], v[10:11], off sc0 nt
	global_load_dwordx4 v[78:81], v[12:13], off sc0 nt
	v_add_co_u32_e32 v10, vcc, s0, v162
	s_mov_b32 s0, 0xe0e000
	s_nop 0
	v_addc_co_u32_e32 v11, vcc, 0, v163, vcc
	v_add_co_u32_e32 v12, vcc, s0, v162
	s_mov_b32 s0, 0xe10000
	s_nop 0
	v_addc_co_u32_e32 v13, vcc, 0, v163, vcc
	global_load_dwordx4 v[102:105], v[10:11], off sc0 nt
	global_load_dwordx4 v[110:113], v[12:13], off sc0 nt
	v_add_co_u32_e32 v10, vcc, s0, v162
	s_mov_b32 s0, 0xe12000
	s_nop 0
	v_addc_co_u32_e32 v11, vcc, 0, v163, vcc
	v_add_co_u32_e32 v12, vcc, s0, v162
	s_mov_b32 s0, 0xe14000
	s_nop 0
	v_addc_co_u32_e32 v13, vcc, 0, v163, vcc
	global_load_dwordx4 v[38:41], v[10:11], off sc0 nt
	global_load_dwordx4 v[46:49], v[12:13], off sc0 nt
	v_add_co_u32_e32 v10, vcc, s0, v162
	s_mov_b32 s0, 0xe16000
	s_nop 0
	v_addc_co_u32_e32 v11, vcc, 0, v163, vcc
	v_add_co_u32_e32 v12, vcc, s0, v162
	s_mov_b32 s0, 0xe18000
	s_nop 0
	v_addc_co_u32_e32 v13, vcc, 0, v163, vcc
	global_load_dwordx4 v[74:77], v[10:11], off sc0 nt
	global_load_dwordx4 v[82:85], v[12:13], off sc0 nt
	v_add_co_u32_e32 v10, vcc, s0, v162
	s_mov_b32 s0, 0xe1a000
	s_nop 0
	v_addc_co_u32_e32 v11, vcc, 0, v163, vcc
	v_add_co_u32_e32 v14, vcc, s0, v162
	s_mov_b32 s0, 0xe1c000
	s_nop 0
	v_addc_co_u32_e32 v15, vcc, 0, v163, vcc
	v_add_co_u32_e32 v42, vcc, s0, v162
	s_mov_b32 s0, 0xe1e000
	s_nop 0
	v_addc_co_u32_e32 v43, vcc, 0, v163, vcc
	v_add_co_u32_e32 v50, vcc, s0, v162
	global_load_dwordx4 v[10:13], v[10:11], off sc0 nt
	s_nop 0
	global_load_dwordx4 v[14:17], v[14:15], off sc0 nt
	v_addc_co_u32_e32 v51, vcc, 0, v163, vcc
	global_load_dwordx4 v[42:45], v[42:43], off sc0 nt
	s_nop 0
	global_load_dwordx4 v[50:53], v[50:51], off sc0 nt
	ds_read_b128 v[130:133], v142 offset:34816
	s_waitcnt lgkmcnt(0)
	global_store_dwordx4 v[144:145], v[130:133], off offset:1280 nt
	ds_read_b128 v[130:133], v146 offset:34816
	s_waitcnt lgkmcnt(0)
	global_store_dwordx4 v[148:149], v[130:133], off offset:1280 nt
	ds_read_b128 v[130:133], v150 offset:34816
	s_waitcnt lgkmcnt(0)
	global_store_dwordx4 v[152:153], v[130:133], off offset:1280 nt
	ds_read_b128 v[130:133], v158 offset:34816
	s_waitcnt lgkmcnt(0)
	global_store_dwordx4 v[160:161], v[130:133], off offset:1280 nt
	s_waitcnt vmcnt(39)
	v_mul_f32_e32 v86, 0x43800000, v86
	s_waitcnt vmcnt(38)
	v_mul_f32_e32 v94, 0x43800000, v94
	s_waitcnt vmcnt(35)
	v_mul_f32_e32 v54, 0x43800000, v54
	s_waitcnt vmcnt(34)
	v_mul_f32_e32 v62, 0x43800000, v62
	s_waitcnt vmcnt(31)
	v_mul_f32_e32 v22, 0x43800000, v22
	s_waitcnt vmcnt(30)
	v_mul_f32_e32 v30, 0x43800000, v30
	s_waitcnt vmcnt(27)
	v_mul_f32_e32 v2, 0x43800000, v2
	s_waitcnt vmcnt(26)
	v_mul_f32_e32 v6, 0x43800000, v6
	v_med3_f32 v86, v86, s85, v252
	v_med3_f32 v94, v94, s85, v252
	v_mov_b32_e32 v130, v155
	v_med3_f32 v54, v54, s85, v252
	v_med3_f32 v62, v62, s85, v252
	v_mov_b32_e32 v131, v155
	v_med3_f32 v22, v22, s85, v252
	v_med3_f32 v30, v30, s85, v252
	v_mov_b32_e32 v132, v155
	v_med3_f32 v2, v2, s85, v252
	v_med3_f32 v6, v6, s85, v252
	v_mov_b32_e32 v133, v155
	v_cvt_pk_fp8_f32 v130, v86, v94
	v_cvt_pk_fp8_f32 v131, v54, v62
	v_cvt_pk_fp8_f32 v132, v22, v30
	v_cvt_pk_fp8_f32 v133, v2, v6
	v_mul_f32_e32 v114, 0x43800000, v114
	v_mul_f32_e32 v118, 0x43800000, v118
	v_mul_f32_e32 v70, 0x43800000, v70
	v_mul_f32_e32 v86, 0x43800000, v90
	v_mul_f32_e32 v34, 0x43800000, v34
	v_mul_f32_e32 v54, 0x43800000, v58
	s_waitcnt vmcnt(25)
	v_mul_f32_e32 v18, 0x43800000, v18
	s_waitcnt vmcnt(24)
	v_mul_f32_e32 v22, 0x43800000, v26
	v_med3_f32 v114, v114, s85, v252
	v_med3_f32 v118, v118, s85, v252
	v_med3_f32 v70, v70, s85, v252
	v_med3_f32 v86, v86, s85, v252
	v_med3_f32 v34, v34, s85, v252
	v_med3_f32 v54, v54, s85, v252
	v_med3_f32 v18, v18, s85, v252
	v_med3_f32 v22, v22, s85, v252
	v_cvt_pk_fp8_f32 v130, v114, v118 op_sel:[0,0,1]
	v_cvt_pk_fp8_f32 v131, v70, v86 op_sel:[0,0,1]
	v_cvt_pk_fp8_f32 v132, v34, v54 op_sel:[0,0,1]
	v_cvt_pk_fp8_f32 v133, v18, v22 op_sel:[0,0,1]
	v_mul_f32_e32 v2, 0x43800000, v87
	v_mul_f32_e32 v6, 0x43800000, v95
	v_med3_f32 v2, v2, s85, v252
	ds_write_b128 v164, v[130:133]
	v_med3_f32 v6, v6, s85, v252
	v_mov_b32_e32 v130, v155
	v_cvt_pk_fp8_f32 v130, v2, v6
	v_mul_f32_e32 v2, 0x43800000, v55
	v_mul_f32_e32 v6, 0x43800000, v63
	v_med3_f32 v2, v2, s85, v252
	v_med3_f32 v6, v6, s85, v252
	v_mov_b32_e32 v131, v155
	v_cvt_pk_fp8_f32 v131, v2, v6
	v_mul_f32_e32 v2, 0x43800000, v23
	v_mul_f32_e32 v6, 0x43800000, v31
	v_med3_f32 v2, v2, s85, v252
	v_med3_f32 v6, v6, s85, v252
	v_mov_b32_e32 v132, v155
	v_mul_f32_e32 v18, 0x43800000, v115
	v_mul_f32_e32 v22, 0x43800000, v119
	v_cvt_pk_fp8_f32 v132, v2, v6
	v_mul_f32_e32 v2, 0x43800000, v3
	v_mul_f32_e32 v3, 0x43800000, v7
	v_med3_f32 v18, v18, s85, v252
	v_med3_f32 v22, v22, s85, v252
	v_med3_f32 v2, v2, s85, v252
	v_med3_f32 v3, v3, s85, v252
	v_mov_b32_e32 v133, v155
	v_cvt_pk_fp8_f32 v130, v18, v22 op_sel:[0,0,1]
	v_mul_f32_e32 v18, 0x43800000, v71
	v_mul_f32_e32 v22, 0x43800000, v91
	v_cvt_pk_fp8_f32 v133, v2, v3
	v_med3_f32 v18, v18, s85, v252
	v_med3_f32 v22, v22, s85, v252
	v_cvt_pk_fp8_f32 v131, v18, v22 op_sel:[0,0,1]
	v_mul_f32_e32 v18, 0x43800000, v35
	v_mul_f32_e32 v22, 0x43800000, v59
	v_mul_f32_e32 v6, 0x43800000, v19
	v_mul_f32_e32 v7, 0x43800000, v27
	v_med3_f32 v18, v18, s85, v252
	v_med3_f32 v22, v22, s85, v252
	v_med3_f32 v6, v6, s85, v252
	v_med3_f32 v7, v7, s85, v252
	v_cvt_pk_fp8_f32 v132, v18, v22 op_sel:[0,0,1]
	v_cvt_pk_fp8_f32 v133, v6, v7 op_sel:[0,0,1]
	v_mul_f32_e32 v2, 0x43800000, v88
	v_mul_f32_e32 v3, 0x43800000, v96
	v_med3_f32 v2, v2, s85, v252
	ds_write_b128 v164, v[130:133] offset:272
	v_med3_f32 v3, v3, s85, v252
	v_mov_b32_e32 v130, v155
	v_cvt_pk_fp8_f32 v130, v2, v3
	v_mul_f32_e32 v2, 0x43800000, v56
	v_mul_f32_e32 v3, 0x43800000, v64
	v_med3_f32 v2, v2, s85, v252
	v_med3_f32 v3, v3, s85, v252
	v_mov_b32_e32 v131, v155
	v_mul_f32_e32 v6, 0x43800000, v116
	v_mul_f32_e32 v7, 0x43800000, v120
	v_cvt_pk_fp8_f32 v131, v2, v3
	v_mul_f32_e32 v2, 0x43800000, v24
	v_mul_f32_e32 v3, 0x43800000, v32
	v_med3_f32 v6, v6, s85, v252
	v_med3_f32 v7, v7, s85, v252
	v_med3_f32 v2, v2, s85, v252
	v_med3_f32 v3, v3, s85, v252
	v_mov_b32_e32 v132, v155
	v_cvt_pk_fp8_f32 v130, v6, v7 op_sel:[0,0,1]
	v_mul_f32_e32 v6, 0x43800000, v72
	v_mul_f32_e32 v7, 0x43800000, v92
	v_cvt_pk_fp8_f32 v132, v2, v3
	v_med3_f32 v6, v6, s85, v252
	v_med3_f32 v7, v7, s85, v252
	v_mul_f32_e32 v2, 0x43800000, v4
	v_mul_f32_e32 v3, 0x43800000, v8
	v_cvt_pk_fp8_f32 v131, v6, v7 op_sel:[0,0,1]
	v_mul_f32_e32 v6, 0x43800000, v36
	v_mul_f32_e32 v7, 0x43800000, v60
	v_med3_f32 v2, v2, s85, v252
	v_med3_f32 v3, v3, s85, v252
	v_mov_b32_e32 v133, v155
	v_med3_f32 v6, v6, s85, v252
	v_med3_f32 v7, v7, s85, v252
	v_cvt_pk_fp8_f32 v133, v2, v3
	v_mul_f32_e32 v2, 0x43800000, v89
	v_mul_f32_e32 v3, 0x43800000, v97
	v_cvt_pk_fp8_f32 v132, v6, v7 op_sel:[0,0,1]
	v_med3_f32 v7, v2, s85, v252
	v_med3_f32 v3, v3, s85, v252
	v_mov_b32_e32 v2, v155
	v_mul_f32_e32 v4, 0x43800000, v20
	v_mul_f32_e32 v6, 0x43800000, v28
	v_cvt_pk_fp8_f32 v2, v7, v3
	v_med3_f32 v4, v4, s85, v252
	v_med3_f32 v6, v6, s85, v252
	v_cvt_pk_fp8_f32 v133, v4, v6 op_sel:[0,0,1]
	v_mul_f32_e32 v4, 0x43800000, v117
	v_mul_f32_e32 v6, 0x43800000, v121
	v_med3_f32 v4, v4, s85, v252
	v_med3_f32 v6, v6, s85, v252
	v_cvt_pk_fp8_f32 v2, v4, v6 op_sel:[0,0,1]
	v_mul_f32_e32 v3, 0x43800000, v57
	v_mul_f32_e32 v4, 0x43800000, v65
	v_med3_f32 v8, v3, s85, v252
	v_med3_f32 v4, v4, s85, v252
	v_mov_b32_e32 v3, v155
	v_cvt_pk_fp8_f32 v3, v8, v4
	v_mul_f32_e32 v6, 0x43800000, v73
	v_mul_f32_e32 v7, 0x43800000, v93
	v_med3_f32 v6, v6, s85, v252
	v_med3_f32 v7, v7, s85, v252
	v_cvt_pk_fp8_f32 v3, v6, v7 op_sel:[0,0,1]
	v_mul_f32_e32 v4, 0x43800000, v25
	v_mul_f32_e32 v6, 0x43800000, v33
	v_med3_f32 v18, v4, s85, v252
	v_med3_f32 v6, v6, s85, v252
	v_mov_b32_e32 v4, v155
	v_cvt_pk_fp8_f32 v4, v18, v6
	v_mul_f32_e32 v5, 0x43800000, v5
	v_mul_f32_e32 v6, 0x43800000, v9
	v_med3_f32 v9, v5, s85, v252
	v_med3_f32 v6, v6, s85, v252
	v_mov_b32_e32 v5, v155
	v_mul_f32_e32 v7, 0x43800000, v37
	v_mul_f32_e32 v8, 0x43800000, v61
	v_cvt_pk_fp8_f32 v5, v9, v6
	v_med3_f32 v7, v7, s85, v252
	v_med3_f32 v8, v8, s85, v252
	v_cvt_pk_fp8_f32 v4, v7, v8 op_sel:[0,0,1]
	v_mul_f32_e32 v7, 0x43800000, v21
	v_mul_f32_e32 v8, 0x43800000, v29
	v_med3_f32 v7, v7, s85, v252
	v_med3_f32 v8, v8, s85, v252
	v_cvt_pk_fp8_f32 v5, v7, v8 op_sel:[0,0,1]
	ds_write_b128 v164, v[130:133] offset:544
	ds_write_b128 v164, v[2:5] offset:816
	s_waitcnt lgkmcnt(0)
	s_barrier
	ds_read_b128 v[2:5], v142
	s_waitcnt lgkmcnt(0)
	global_store_dwordx4 v[144:145], v[2:5], off offset:1536 nt
	ds_read_b128 v[2:5], v146
	s_waitcnt lgkmcnt(0)
	global_store_dwordx4 v[148:149], v[2:5], off offset:1536 nt
	ds_read_b128 v[2:5], v150
	s_waitcnt lgkmcnt(0)
	global_store_dwordx4 v[152:153], v[2:5], off offset:1536 nt
	ds_read_b128 v[2:5], v158
	s_waitcnt lgkmcnt(0)
	global_store_dwordx4 v[160:161], v[2:5], off offset:1536 nt
	s_waitcnt vmcnt(23)
	s_nop 0
	v_mul_f32_e32 v2, 0x43800000, v98
	s_waitcnt vmcnt(22)
	v_mul_f32_e32 v3, 0x43800000, v106
	v_med3_f32 v6, v2, s85, v252
	v_med3_f32 v3, v3, s85, v252
	v_mov_b32_e32 v2, v155
	v_cvt_pk_fp8_f32 v2, v6, v3
	s_waitcnt vmcnt(21)
	v_mul_f32_e32 v4, 0x43800000, v122
	s_waitcnt vmcnt(20)
	v_mul_f32_e32 v5, 0x43800000, v126
	v_med3_f32 v4, v4, s85, v252
	v_med3_f32 v5, v5, s85, v252
	v_cvt_pk_fp8_f32 v2, v4, v5 op_sel:[0,0,1]
	s_waitcnt vmcnt(19)
	v_mul_f32_e32 v3, 0x43800000, v66
	s_waitcnt vmcnt(18)
	v_mul_f32_e32 v4, 0x43800000, v78
	v_med3_f32 v7, v3, s85, v252
	v_med3_f32 v4, v4, s85, v252
	v_mov_b32_e32 v3, v155
	v_cvt_pk_fp8_f32 v3, v7, v4
	s_waitcnt vmcnt(17)
	v_mul_f32_e32 v5, 0x43800000, v102
	s_waitcnt vmcnt(16)
	v_mul_f32_e32 v6, 0x43800000, v110
	v_med3_f32 v5, v5, s85, v252
	v_med3_f32 v6, v6, s85, v252
	v_cvt_pk_fp8_f32 v3, v5, v6 op_sel:[0,0,1]
	s_waitcnt vmcnt(15)
	v_mul_f32_e32 v4, 0x43800000, v38
	s_waitcnt vmcnt(14)
	v_mul_f32_e32 v5, 0x43800000, v46
	v_med3_f32 v8, v4, s85, v252
	v_med3_f32 v5, v5, s85, v252
	v_mov_b32_e32 v4, v155
	v_cvt_pk_fp8_f32 v4, v8, v5
	s_waitcnt vmcnt(13)
	v_mul_f32_e32 v6, 0x43800000, v74
	s_waitcnt vmcnt(12)
	v_mul_f32_e32 v7, 0x43800000, v82
	v_med3_f32 v6, v6, s85, v252
	v_med3_f32 v7, v7, s85, v252
	v_cvt_pk_fp8_f32 v4, v6, v7 op_sel:[0,0,1]
	s_waitcnt vmcnt(11)
	v_mul_f32_e32 v5, 0x43800000, v10
	s_waitcnt vmcnt(10)
	v_mul_f32_e32 v6, 0x43800000, v14
	v_med3_f32 v9, v5, s85, v252
	v_med3_f32 v6, v6, s85, v252
	v_mov_b32_e32 v5, v155
	v_cvt_pk_fp8_f32 v5, v9, v6
	s_waitcnt vmcnt(9)
	v_mul_f32_e32 v7, 0x43800000, v42
	s_waitcnt vmcnt(8)
	v_mul_f32_e32 v8, 0x43800000, v50
	v_med3_f32 v7, v7, s85, v252
	v_med3_f32 v8, v8, s85, v252
	v_cvt_pk_fp8_f32 v5, v7, v8 op_sel:[0,0,1]
	ds_write_b128 v164, v[2:5] offset:34816
	v_mul_f32_e32 v2, 0x43800000, v99
	v_mul_f32_e32 v3, 0x43800000, v107
	v_med3_f32 v6, v2, s85, v252
	v_med3_f32 v3, v3, s85, v252
	v_mov_b32_e32 v2, v155
	v_cvt_pk_fp8_f32 v2, v6, v3
	v_mul_f32_e32 v4, 0x43800000, v123
	v_mul_f32_e32 v5, 0x43800000, v127
	v_med3_f32 v4, v4, s85, v252
	v_med3_f32 v5, v5, s85, v252
	v_cvt_pk_fp8_f32 v2, v4, v5 op_sel:[0,0,1]
	v_mul_f32_e32 v3, 0x43800000, v67
	v_mul_f32_e32 v4, 0x43800000, v79
	v_med3_f32 v7, v3, s85, v252
	v_med3_f32 v4, v4, s85, v252
	v_mov_b32_e32 v3, v155
	v_cvt_pk_fp8_f32 v3, v7, v4
	v_mul_f32_e32 v5, 0x43800000, v103
	v_mul_f32_e32 v6, 0x43800000, v111
	v_med3_f32 v5, v5, s85, v252
	v_med3_f32 v6, v6, s85, v252
	v_cvt_pk_fp8_f32 v3, v5, v6 op_sel:[0,0,1]
	v_mul_f32_e32 v4, 0x43800000, v39
	v_mul_f32_e32 v5, 0x43800000, v47
	v_med3_f32 v8, v4, s85, v252
	v_med3_f32 v5, v5, s85, v252
	v_mov_b32_e32 v4, v155
	v_cvt_pk_fp8_f32 v4, v8, v5
	v_mul_f32_e32 v6, 0x43800000, v75
	v_mul_f32_e32 v7, 0x43800000, v83
	v_med3_f32 v6, v6, s85, v252
	v_med3_f32 v7, v7, s85, v252
	v_cvt_pk_fp8_f32 v4, v6, v7 op_sel:[0,0,1]
	v_mul_f32_e32 v5, 0x43800000, v11
	v_mul_f32_e32 v6, 0x43800000, v15
	v_med3_f32 v9, v5, s85, v252
	v_med3_f32 v6, v6, s85, v252
	v_mov_b32_e32 v5, v155
	v_cvt_pk_fp8_f32 v5, v9, v6
	v_mul_f32_e32 v7, 0x43800000, v43
	v_mul_f32_e32 v8, 0x43800000, v51
	v_med3_f32 v7, v7, s85, v252
	v_med3_f32 v8, v8, s85, v252
	v_cvt_pk_fp8_f32 v5, v7, v8 op_sel:[0,0,1]
	ds_write_b128 v164, v[2:5] offset:35088
	v_mul_f32_e32 v2, 0x43800000, v100
	v_mul_f32_e32 v3, 0x43800000, v108
	v_med3_f32 v6, v2, s85, v252
	v_med3_f32 v3, v3, s85, v252
	v_mov_b32_e32 v2, v155
	v_cvt_pk_fp8_f32 v2, v6, v3
	v_mul_f32_e32 v4, 0x43800000, v124
	v_mul_f32_e32 v5, 0x43800000, v128
	v_med3_f32 v4, v4, s85, v252
	v_med3_f32 v5, v5, s85, v252
	v_cvt_pk_fp8_f32 v2, v4, v5 op_sel:[0,0,1]
	v_mul_f32_e32 v3, 0x43800000, v68
	v_mul_f32_e32 v4, 0x43800000, v80
	v_med3_f32 v7, v3, s85, v252
	v_med3_f32 v4, v4, s85, v252
	v_mov_b32_e32 v3, v155
	v_cvt_pk_fp8_f32 v3, v7, v4
	v_mul_f32_e32 v5, 0x43800000, v104
	v_mul_f32_e32 v6, 0x43800000, v112
	v_med3_f32 v5, v5, s85, v252
	v_med3_f32 v6, v6, s85, v252
	v_cvt_pk_fp8_f32 v3, v5, v6 op_sel:[0,0,1]
	v_mul_f32_e32 v4, 0x43800000, v40
	v_mul_f32_e32 v5, 0x43800000, v48
	v_med3_f32 v8, v4, s85, v252
	v_med3_f32 v5, v5, s85, v252
	v_mov_b32_e32 v4, v155
	v_cvt_pk_fp8_f32 v4, v8, v5
	v_mul_f32_e32 v6, 0x43800000, v76
	v_mul_f32_e32 v7, 0x43800000, v84
	v_med3_f32 v6, v6, s85, v252
	v_med3_f32 v7, v7, s85, v252
	v_cvt_pk_fp8_f32 v4, v6, v7 op_sel:[0,0,1]
	v_mul_f32_e32 v5, 0x43800000, v12
	v_mul_f32_e32 v6, 0x43800000, v16
	v_med3_f32 v9, v5, s85, v252
	v_med3_f32 v6, v6, s85, v252
	v_mov_b32_e32 v5, v155
	v_cvt_pk_fp8_f32 v5, v9, v6
	v_mul_f32_e32 v7, 0x43800000, v44
	v_mul_f32_e32 v8, 0x43800000, v52
	v_med3_f32 v7, v7, s85, v252
	v_med3_f32 v8, v8, s85, v252
	v_cvt_pk_fp8_f32 v5, v7, v8 op_sel:[0,0,1]
	ds_write_b128 v164, v[2:5] offset:35360
	v_mul_f32_e32 v2, 0x43800000, v101
	v_mul_f32_e32 v3, 0x43800000, v109
	v_med3_f32 v6, v2, s85, v252
	v_med3_f32 v3, v3, s85, v252
	v_mov_b32_e32 v2, v155
	v_cvt_pk_fp8_f32 v2, v6, v3
	v_mul_f32_e32 v4, 0x43800000, v125
	v_mul_f32_e32 v5, 0x43800000, v129
	v_med3_f32 v4, v4, s85, v252
	v_med3_f32 v5, v5, s85, v252
	v_cvt_pk_fp8_f32 v2, v4, v5 op_sel:[0,0,1]
	v_mul_f32_e32 v3, 0x43800000, v69
	v_mul_f32_e32 v4, 0x43800000, v81
	v_med3_f32 v7, v3, s85, v252
	v_med3_f32 v4, v4, s85, v252
	v_mov_b32_e32 v3, v155
	v_cvt_pk_fp8_f32 v3, v7, v4
	v_mul_f32_e32 v5, 0x43800000, v105
	v_mul_f32_e32 v6, 0x43800000, v113
	v_med3_f32 v5, v5, s85, v252
	v_med3_f32 v6, v6, s85, v252
	v_cvt_pk_fp8_f32 v3, v5, v6 op_sel:[0,0,1]
	v_mul_f32_e32 v4, 0x43800000, v41
	v_mul_f32_e32 v5, 0x43800000, v49
	v_med3_f32 v8, v4, s85, v252
	v_med3_f32 v5, v5, s85, v252
	v_mov_b32_e32 v4, v155
	v_cvt_pk_fp8_f32 v4, v8, v5
	v_mul_f32_e32 v6, 0x43800000, v77
	v_mul_f32_e32 v7, 0x43800000, v85
	v_med3_f32 v6, v6, s85, v252
	v_med3_f32 v7, v7, s85, v252
	v_cvt_pk_fp8_f32 v4, v6, v7 op_sel:[0,0,1]
	v_mul_f32_e32 v5, 0x43800000, v13
	v_mul_f32_e32 v6, 0x43800000, v17
	v_med3_f32 v9, v5, s85, v252
	v_med3_f32 v6, v6, s85, v252
	v_mov_b32_e32 v5, v155
	v_cvt_pk_fp8_f32 v5, v9, v6
	v_mul_f32_e32 v7, 0x43800000, v45
	v_mul_f32_e32 v8, 0x43800000, v53
	v_med3_f32 v7, v7, s85, v252
	v_med3_f32 v8, v8, s85, v252
	v_cvt_pk_fp8_f32 v5, v7, v8 op_sel:[0,0,1]
	ds_write_b128 v164, v[2:5] offset:35632
	s_waitcnt lgkmcnt(0)
	s_barrier
	ds_read_b128 v[2:5], v142 offset:34816
	s_waitcnt lgkmcnt(0)
	global_store_dwordx4 v[144:145], v[2:5], off offset:1792 nt
	ds_read_b128 v[2:5], v146 offset:34816
	s_waitcnt lgkmcnt(0)
	global_store_dwordx4 v[148:149], v[2:5], off offset:1792 nt
	ds_read_b128 v[2:5], v150 offset:34816
	s_waitcnt lgkmcnt(0)
	global_store_dwordx4 v[152:153], v[2:5], off offset:1792 nt
	ds_read_b128 v[2:5], v158 offset:34816
	s_waitcnt lgkmcnt(0)
	global_store_dwordx4 v[160:161], v[2:5], off offset:1792 nt
	s_barrier
	s_mov_b64 s[30:31], 0
.LBB0_170:
	s_andn2_b64 vcc, exec, s[30:31]
	s_cbranch_vccnz .LBB0_172
	s_ashr_i32 s0, s4, 5
	s_ashr_i32 s1, s0, 31
	v_readlane_b32 s56, v254, 4
	s_and_b32 s10, s4, 31
	s_lshl_b64 s[6:7], s[0:1], 25
	v_readlane_b32 s58, v254, 6
	v_readlane_b32 s59, v254, 7
	s_add_u32 s6, s58, s6
	s_addc_u32 s7, s59, s7
	s_lshl_b32 s12, s4, 6
	s_lshl_b32 s30, s4, 11
	s_and_b32 s12, s12, 0x780
	s_and_b32 s30, s30, 0x800
	s_or_b32 s12, s12, s30
	s_lshl_b32 s12, s12, 2
	s_add_u32 s6, s6, s12
	s_addc_u32 s7, s7, 0
	s_lshl_b32 s10, s10, 18
	s_lshl_b64 s[0:1], s[0:1], 23
	s_add_u32 s0, s53, s0
	v_readlane_b32 s2, v255, 5
	v_mov_b32_e32 v130, v0
	s_addc_u32 s1, s2, s1
	s_add_u32 s30, s0, s10
	v_readfirstlane_b32 s11, v130
	s_addc_u32 s31, s1, 0
	s_ashr_i32 s0, s11, 1
	v_lshrrev_b32_e32 v2, 1, v130
	s_andn2_b32 s0, s0, 31
	v_and_b32_e32 v131, 16, v2
	v_or_b32_e32 v2, s0, v131
	v_ashrrev_i32_e32 v3, 31, v2
	s_waitcnt lgkmcnt(0)
	v_lshlrev_b32_e32 v4, 2, v130
	v_lshlrev_b64 v[2:3], 14, v[2:3]
	v_and_b32_e32 v136, 0x7c, v4
	v_lshl_add_u64 v[2:3], s[6:7], 0, v[2:3]
	v_lshlrev_b32_e32 v154, 2, v136
	v_lshl_add_u64 v[162:163], v[2:3], 0, v[154:155]
	v_add_co_u32_e32 v2, vcc, s35, v162
	s_mov_b32 s1, 0x20000
	s_nop 0
	v_addc_co_u32_e32 v3, vcc, 0, v163, vcc
	global_load_dwordx4 v[98:101], v[162:163], off sc0 nt
	global_load_dwordx4 v[102:105], v[2:3], off sc0 nt
	v_add_co_u32_e32 v2, vcc, s36, v162
	v_readlane_b32 s57, v254, 5
	s_nop 0
	v_addc_co_u32_e32 v3, vcc, 0, v163, vcc
	v_add_co_u32_e32 v4, vcc, s37, v162
	v_readlane_b32 s60, v254, 8
	s_nop 0
	v_addc_co_u32_e32 v5, vcc, 0, v163, vcc
	global_load_dwordx4 v[114:117], v[2:3], off sc0 nt
	global_load_dwordx4 v[118:121], v[4:5], off sc0 nt
	v_add_co_u32_e32 v2, vcc, s38, v162
	v_readlane_b32 s61, v254, 9
	s_nop 0
	v_addc_co_u32_e32 v3, vcc, 0, v163, vcc
	v_add_co_u32_e32 v4, vcc, s39, v162
	v_readlane_b32 s62, v254, 10
	s_nop 0
	v_addc_co_u32_e32 v5, vcc, 0, v163, vcc
	global_load_dwordx4 v[54:57], v[2:3], off sc0 nt
	global_load_dwordx4 v[66:69], v[4:5], off sc0 nt
	v_add_co_u32_e32 v2, vcc, s40, v162
	v_readlane_b32 s63, v254, 11
	s_nop 0
	v_addc_co_u32_e32 v3, vcc, 0, v163, vcc
	v_add_co_u32_e32 v4, vcc, s41, v162
	s_nop 1
	v_addc_co_u32_e32 v5, vcc, 0, v163, vcc
	global_load_dwordx4 v[82:85], v[2:3], off sc0 nt
	global_load_dwordx4 v[86:89], v[4:5], off sc0 nt
	v_add_co_u32_e32 v2, vcc, s1, v162
	s_mov_b32 s1, 0x24000
	s_nop 0
	v_addc_co_u32_e32 v3, vcc, 0, v163, vcc
	v_add_co_u32_e32 v4, vcc, s1, v162
	s_mov_b32 s1, 0x28000
	s_nop 0
	v_addc_co_u32_e32 v5, vcc, 0, v163, vcc
	global_load_dwordx4 v[18:21], v[2:3], off sc0 nt
	global_load_dwordx4 v[26:29], v[4:5], off sc0 nt
	v_add_co_u32_e32 v2, vcc, s1, v162
	s_mov_b32 s1, 0x2c000
	s_nop 0
	v_addc_co_u32_e32 v3, vcc, 0, v163, vcc
	v_add_co_u32_e32 v4, vcc, s1, v162
	s_mov_b32 s1, 0x30000
	s_nop 0
	v_addc_co_u32_e32 v5, vcc, 0, v163, vcc
	global_load_dwordx4 v[50:53], v[2:3], off sc0 nt
	global_load_dwordx4 v[58:61], v[4:5], off sc0 nt
	v_add_co_u32_e32 v2, vcc, s1, v162
	s_mov_b32 s1, 0x34000
	s_nop 0
	v_addc_co_u32_e32 v3, vcc, 0, v163, vcc
	v_add_co_u32_e32 v6, vcc, s1, v162
	s_mov_b32 s1, 0x38000
	s_nop 0
	v_addc_co_u32_e32 v7, vcc, 0, v163, vcc
	v_add_co_u32_e32 v10, vcc, s1, v162
	s_mov_b32 s1, 0x3c000
	s_nop 0
	v_addc_co_u32_e32 v11, vcc, 0, v163, vcc
	v_add_co_u32_e32 v12, vcc, s1, v162
	global_load_dwordx4 v[2:5], v[2:3], off sc0 nt
	s_nop 0
	global_load_dwordx4 v[6:9], v[6:7], off sc0 nt
	v_addc_co_u32_e32 v13, vcc, 0, v163, vcc
	global_load_dwordx4 v[22:25], v[10:11], off sc0 nt
	global_load_dwordx4 v[34:37], v[12:13], off sc0 nt
	v_add_co_u32_e32 v10, vcc, s43, v162
	s_mov_b32 s1, 0x420000
	s_nop 0
	v_addc_co_u32_e32 v11, vcc, 0, v163, vcc
	v_add_co_u32_e32 v12, vcc, s44, v162
	s_nop 1
	v_addc_co_u32_e32 v13, vcc, 0, v163, vcc
	global_load_dwordx4 v[106:109], v[10:11], off sc0 nt
	global_load_dwordx4 v[110:113], v[12:13], off sc0 nt
	v_add_co_u32_e32 v10, vcc, s45, v162
	s_nop 1
	v_addc_co_u32_e32 v11, vcc, 0, v163, vcc
	v_add_co_u32_e32 v12, vcc, s46, v162
	s_nop 1
	v_addc_co_u32_e32 v13, vcc, 0, v163, vcc
	global_load_dwordx4 v[122:125], v[10:11], off sc0 nt
	global_load_dwordx4 v[126:129], v[12:13], off sc0 nt
	v_add_co_u32_e32 v10, vcc, s47, v162
	s_nop 1
	v_addc_co_u32_e32 v11, vcc, 0, v163, vcc
	v_add_co_u32_e32 v12, vcc, s48, v162
	s_nop 1
	v_addc_co_u32_e32 v13, vcc, 0, v163, vcc
	global_load_dwordx4 v[70:73], v[10:11], off sc0 nt
	global_load_dwordx4 v[78:81], v[12:13], off sc0 nt
	v_add_co_u32_e32 v10, vcc, s49, v162
	s_nop 1
	v_addc_co_u32_e32 v11, vcc, 0, v163, vcc
	v_add_co_u32_e32 v12, vcc, s52, v162
	s_nop 1
	v_addc_co_u32_e32 v13, vcc, 0, v163, vcc
	global_load_dwordx4 v[90:93], v[10:11], off sc0 nt
	global_load_dwordx4 v[94:97], v[12:13], off sc0 nt
	v_add_co_u32_e32 v10, vcc, s1, v162
	s_mov_b32 s1, 0x424000
	s_nop 0
	v_addc_co_u32_e32 v11, vcc, 0, v163, vcc
	v_add_co_u32_e32 v12, vcc, s1, v162
	s_mov_b32 s1, 0x428000
	s_nop 0
	v_addc_co_u32_e32 v13, vcc, 0, v163, vcc
	global_load_dwordx4 v[30:33], v[10:11], off sc0 nt
	global_load_dwordx4 v[42:45], v[12:13], off sc0 nt
	v_add_co_u32_e32 v10, vcc, s1, v162
	s_mov_b32 s1, 0x42c000
	s_nop 0
	v_addc_co_u32_e32 v11, vcc, 0, v163, vcc
	v_add_co_u32_e32 v12, vcc, s1, v162
	s_mov_b32 s1, 0x430000
	s_nop 0
	v_addc_co_u32_e32 v13, vcc, 0, v163, vcc
	global_load_dwordx4 v[62:65], v[10:11], off sc0 nt
	global_load_dwordx4 v[74:77], v[12:13], off sc0 nt
	v_add_co_u32_e32 v10, vcc, s1, v162
	s_mov_b32 s1, 0x434000
	s_nop 0
	v_addc_co_u32_e32 v11, vcc, 0, v163, vcc
	v_add_co_u32_e32 v14, vcc, s1, v162
	s_mov_b32 s1, 0x438000
	s_nop 0
	v_addc_co_u32_e32 v15, vcc, 0, v163, vcc
	v_add_co_u32_e32 v38, vcc, s1, v162
	s_mov_b32 s1, 0x43c000
	s_nop 0
	v_addc_co_u32_e32 v39, vcc, 0, v163, vcc
	v_add_co_u32_e32 v46, vcc, s1, v162
	global_load_dwordx4 v[10:13], v[10:11], off sc0 nt
	s_nop 0
	global_load_dwordx4 v[14:17], v[14:15], off sc0 nt
	v_addc_co_u32_e32 v47, vcc, 0, v163, vcc
	global_load_dwordx4 v[38:41], v[38:39], off sc0 nt
	s_nop 0
	global_load_dwordx4 v[46:49], v[46:47], off sc0 nt
	s_waitcnt vmcnt(0)
	v_mul_f32_e32 v98, 0x43800000, v98
	s_waitcnt vmcnt(30)
	v_mul_f32_e32 v102, 0x43800000, v102
	s_waitcnt vmcnt(27)
	v_mul_f32_e32 v54, 0x43800000, v54
	s_waitcnt vmcnt(26)
	v_mul_f32_e32 v66, 0x43800000, v66
	s_waitcnt vmcnt(23)
	v_mul_f32_e32 v18, 0x43800000, v18
	s_waitcnt vmcnt(22)
	v_mul_f32_e32 v26, 0x43800000, v26
	s_waitcnt vmcnt(19)
	v_mul_f32_e32 v2, 0x43800000, v2
	s_waitcnt vmcnt(18)
	v_mul_f32_e32 v6, 0x43800000, v6
	v_med3_f32 v98, v98, s85, v252
	v_med3_f32 v102, v102, s85, v252
	v_mov_b32_e32 v132, v155
	v_med3_f32 v54, v54, s85, v252
	v_med3_f32 v66, v66, s85, v252
	v_mov_b32_e32 v133, v155
	v_med3_f32 v18, v18, s85, v252
	v_med3_f32 v26, v26, s85, v252
	v_mov_b32_e32 v134, v155
	v_med3_f32 v2, v2, s85, v252
	v_med3_f32 v6, v6, s85, v252
	v_mov_b32_e32 v135, v155
	v_cvt_pk_fp8_f32 v132, v98, v102
	v_cvt_pk_fp8_f32 v133, v54, v66
	v_cvt_pk_fp8_f32 v134, v18, v26
	v_cvt_pk_fp8_f32 v135, v2, v6
	v_mul_f32_e32 v114, 0x43800000, v114
	v_mul_f32_e32 v118, 0x43800000, v118
	v_mul_f32_e32 v82, 0x43800000, v82
	v_mul_f32_e32 v86, 0x43800000, v86
	v_mul_f32_e32 v50, 0x43800000, v50
	v_mul_f32_e32 v54, 0x43800000, v58
	s_waitcnt vmcnt(17)
	v_mul_f32_e32 v18, 0x43800000, v22
	s_waitcnt vmcnt(16)
	v_mul_f32_e32 v22, 0x43800000, v34
	v_med3_f32 v114, v114, s85, v252
	v_med3_f32 v118, v118, s85, v252
	v_med3_f32 v82, v82, s85, v252
	v_med3_f32 v86, v86, s85, v252
	v_med3_f32 v50, v50, s85, v252
	v_med3_f32 v54, v54, s85, v252
	v_med3_f32 v18, v18, s85, v252
	v_med3_f32 v22, v22, s85, v252
	v_cvt_pk_fp8_f32 v132, v114, v118 op_sel:[0,0,1]
	v_cvt_pk_fp8_f32 v133, v82, v86 op_sel:[0,0,1]
	v_cvt_pk_fp8_f32 v134, v50, v54 op_sel:[0,0,1]
	v_cvt_pk_fp8_f32 v135, v18, v22 op_sel:[0,0,1]
	s_add_i32 s0, s0, 0
	v_mul_u32_u24_e32 v2, 0x110, v136
	v_add3_u32 v164, s0, v131, v2
	v_mul_f32_e32 v2, 0x43800000, v99
	v_mul_f32_e32 v6, 0x43800000, v103
	ds_write_b128 v164, v[132:135]
	v_med3_f32 v2, v2, s85, v252
	v_med3_f32 v6, v6, s85, v252
	v_mov_b32_e32 v132, v155
	v_cvt_pk_fp8_f32 v132, v2, v6
	v_mul_f32_e32 v2, 0x43800000, v55
	v_mul_f32_e32 v6, 0x43800000, v67
	v_med3_f32 v2, v2, s85, v252
	v_med3_f32 v6, v6, s85, v252
	v_mov_b32_e32 v133, v155
	v_cvt_pk_fp8_f32 v133, v2, v6
	v_mul_f32_e32 v2, 0x43800000, v19
	v_mul_f32_e32 v6, 0x43800000, v27
	v_med3_f32 v2, v2, s85, v252
	v_med3_f32 v6, v6, s85, v252
	v_mov_b32_e32 v134, v155
	v_mul_f32_e32 v18, 0x43800000, v115
	v_mul_f32_e32 v22, 0x43800000, v119
	v_cvt_pk_fp8_f32 v134, v2, v6
	v_mul_f32_e32 v2, 0x43800000, v3
	v_mul_f32_e32 v3, 0x43800000, v7
	v_med3_f32 v18, v18, s85, v252
	v_med3_f32 v22, v22, s85, v252
	v_med3_f32 v2, v2, s85, v252
	v_med3_f32 v3, v3, s85, v252
	v_mov_b32_e32 v135, v155
	v_cvt_pk_fp8_f32 v132, v18, v22 op_sel:[0,0,1]
	v_mul_f32_e32 v18, 0x43800000, v83
	v_mul_f32_e32 v22, 0x43800000, v87
	v_cvt_pk_fp8_f32 v135, v2, v3
	v_med3_f32 v18, v18, s85, v252
	v_med3_f32 v22, v22, s85, v252
	v_cvt_pk_fp8_f32 v133, v18, v22 op_sel:[0,0,1]
	v_mul_f32_e32 v18, 0x43800000, v51
	v_mul_f32_e32 v19, 0x43800000, v59
	v_mul_f32_e32 v6, 0x43800000, v23
	v_mul_f32_e32 v7, 0x43800000, v35
	v_med3_f32 v18, v18, s85, v252
	v_med3_f32 v19, v19, s85, v252
	v_med3_f32 v6, v6, s85, v252
	v_med3_f32 v7, v7, s85, v252
	v_cvt_pk_fp8_f32 v134, v18, v19 op_sel:[0,0,1]
	v_cvt_pk_fp8_f32 v135, v6, v7 op_sel:[0,0,1]
	v_mul_f32_e32 v2, 0x43800000, v100
	v_mul_f32_e32 v3, 0x43800000, v104
	v_med3_f32 v2, v2, s85, v252
	ds_write_b128 v164, v[132:135] offset:272
	v_med3_f32 v3, v3, s85, v252
	v_mov_b32_e32 v132, v155
	v_cvt_pk_fp8_f32 v132, v2, v3
	v_mul_f32_e32 v2, 0x43800000, v56
	v_mul_f32_e32 v3, 0x43800000, v68
	v_med3_f32 v2, v2, s85, v252
	v_med3_f32 v3, v3, s85, v252
	v_mov_b32_e32 v133, v155
	v_mul_f32_e32 v6, 0x43800000, v116
	v_mul_f32_e32 v7, 0x43800000, v120
	v_cvt_pk_fp8_f32 v133, v2, v3
	v_mul_f32_e32 v2, 0x43800000, v20
	v_mul_f32_e32 v3, 0x43800000, v28
	v_med3_f32 v6, v6, s85, v252
	v_med3_f32 v7, v7, s85, v252
	v_med3_f32 v2, v2, s85, v252
	v_med3_f32 v3, v3, s85, v252
	v_mov_b32_e32 v134, v155
	v_cvt_pk_fp8_f32 v132, v6, v7 op_sel:[0,0,1]
	v_mul_f32_e32 v6, 0x43800000, v84
	v_mul_f32_e32 v7, 0x43800000, v88
	v_cvt_pk_fp8_f32 v134, v2, v3
	v_med3_f32 v6, v6, s85, v252
	v_med3_f32 v7, v7, s85, v252
	v_mul_f32_e32 v2, 0x43800000, v4
	v_mul_f32_e32 v3, 0x43800000, v8
	v_cvt_pk_fp8_f32 v133, v6, v7 op_sel:[0,0,1]
	v_mul_f32_e32 v6, 0x43800000, v52
	v_mul_f32_e32 v7, 0x43800000, v60
	v_med3_f32 v2, v2, s85, v252
	v_med3_f32 v3, v3, s85, v252
	v_mov_b32_e32 v135, v155
	v_med3_f32 v6, v6, s85, v252
	v_med3_f32 v7, v7, s85, v252
	v_cvt_pk_fp8_f32 v135, v2, v3
	v_mul_f32_e32 v2, 0x43800000, v101
	v_mul_f32_e32 v3, 0x43800000, v105
	v_cvt_pk_fp8_f32 v134, v6, v7 op_sel:[0,0,1]
	v_med3_f32 v7, v2, s85, v252
	v_med3_f32 v3, v3, s85, v252
	v_mov_b32_e32 v2, v155
	v_mul_f32_e32 v4, 0x43800000, v24
	v_mul_f32_e32 v6, 0x43800000, v36
	v_cvt_pk_fp8_f32 v2, v7, v3
	v_med3_f32 v4, v4, s85, v252
	v_med3_f32 v6, v6, s85, v252
	v_cvt_pk_fp8_f32 v135, v4, v6 op_sel:[0,0,1]
	v_mul_f32_e32 v4, 0x43800000, v117
	v_mul_f32_e32 v6, 0x43800000, v121
	v_med3_f32 v4, v4, s85, v252
	v_med3_f32 v6, v6, s85, v252
	v_cvt_pk_fp8_f32 v2, v4, v6 op_sel:[0,0,1]
	v_mul_f32_e32 v3, 0x43800000, v57
	v_mul_f32_e32 v4, 0x43800000, v69
	v_med3_f32 v8, v3, s85, v252
	v_med3_f32 v4, v4, s85, v252
	v_mov_b32_e32 v3, v155
	v_cvt_pk_fp8_f32 v3, v8, v4
	v_mul_f32_e32 v6, 0x43800000, v85
	v_mul_f32_e32 v7, 0x43800000, v89
	v_med3_f32 v6, v6, s85, v252
	v_med3_f32 v7, v7, s85, v252
	v_cvt_pk_fp8_f32 v3, v6, v7 op_sel:[0,0,1]
	v_mul_f32_e32 v4, 0x43800000, v21
	v_mul_f32_e32 v6, 0x43800000, v29
	v_med3_f32 v18, v4, s85, v252
	v_med3_f32 v6, v6, s85, v252
	v_mov_b32_e32 v4, v155
	v_cvt_pk_fp8_f32 v4, v18, v6
	v_mul_f32_e32 v5, 0x43800000, v5
	v_mul_f32_e32 v6, 0x43800000, v9
	v_med3_f32 v9, v5, s85, v252
	v_med3_f32 v6, v6, s85, v252
	v_mov_b32_e32 v5, v155
	v_mul_f32_e32 v7, 0x43800000, v53
	v_mul_f32_e32 v8, 0x43800000, v61
	v_cvt_pk_fp8_f32 v5, v9, v6
	v_med3_f32 v7, v7, s85, v252
	v_med3_f32 v8, v8, s85, v252
	v_cvt_pk_fp8_f32 v4, v7, v8 op_sel:[0,0,1]
	v_mul_f32_e32 v7, 0x43800000, v25
	v_mul_f32_e32 v8, 0x43800000, v37
	v_med3_f32 v7, v7, s85, v252
	v_med3_f32 v8, v8, s85, v252
	v_cvt_pk_fp8_f32 v5, v7, v8 op_sel:[0,0,1]
	ds_write_b128 v164, v[132:135] offset:544
	v_ashrrev_i32_e32 v132, 4, v130
	v_ashrrev_i32_e32 v133, 31, v132
	ds_write_b128 v164, v[2:5] offset:816
	v_lshlrev_b32_e32 v2, 4, v130
	v_and_b32_e32 v154, 0xf0, v2
	v_add_u32_e32 v2, 0x200, v130
	v_ashrrev_i32_e32 v136, 4, v2
	v_add_u32_e32 v2, 0x400, v130
	v_ashrrev_i32_e32 v140, 4, v2
	v_add_u32_e32 v2, 0x600, v130
	v_ashrrev_i32_e32 v158, 4, v2
	v_ashrrev_i32_e32 v137, 31, v136
	v_ashrrev_i32_e32 v141, 31, v140
	v_ashrrev_i32_e32 v159, 31, v158
	s_waitcnt lgkmcnt(0)
	s_barrier
	v_lshlrev_b64 v[134:135], 11, v[132:133]
	v_lshlrev_b64 v[138:139], 11, v[136:137]
	v_lshlrev_b64 v[152:153], 11, v[140:141]
	v_lshlrev_b64 v[160:161], 11, v[158:159]
	v_add_co_u32_e32 v2, vcc, s84, v162
	s_mov_b32 s0, 0x820000
	s_nop 0
	v_addc_co_u32_e32 v3, vcc, 0, v163, vcc
	v_add_co_u32_e32 v4, vcc, s54, v162
	s_nop 1
	v_addc_co_u32_e32 v5, vcc, 0, v163, vcc
	global_load_dwordx4 v[98:101], v[2:3], off sc0 nt
	global_load_dwordx4 v[102:105], v[4:5], off sc0 nt
	v_add_co_u32_e32 v2, vcc, s55, v162
	s_nop 1
	v_addc_co_u32_e32 v3, vcc, 0, v163, vcc
	v_add_co_u32_e32 v4, vcc, s64, v162
	s_nop 1
	v_addc_co_u32_e32 v5, vcc, 0, v163, vcc
	global_load_dwordx4 v[114:117], v[2:3], off sc0 nt
	global_load_dwordx4 v[118:121], v[4:5], off sc0 nt
	v_add_co_u32_e32 v2, vcc, s65, v162
	s_nop 1
	v_addc_co_u32_e32 v3, vcc, 0, v163, vcc
	v_add_co_u32_e32 v4, vcc, s68, v162
	s_nop 1
	v_addc_co_u32_e32 v5, vcc, 0, v163, vcc
	global_load_dwordx4 v[54:57], v[2:3], off sc0 nt
	global_load_dwordx4 v[66:69], v[4:5], off sc0 nt
	v_add_co_u32_e32 v2, vcc, s69, v162
	s_nop 1
	v_addc_co_u32_e32 v3, vcc, 0, v163, vcc
	v_add_co_u32_e32 v4, vcc, s70, v162
	s_nop 1
	v_addc_co_u32_e32 v5, vcc, 0, v163, vcc
	global_load_dwordx4 v[82:85], v[2:3], off sc0 nt
	global_load_dwordx4 v[86:89], v[4:5], off sc0 nt
	v_add_co_u32_e32 v2, vcc, s0, v162
	s_mov_b32 s0, 0x824000
	s_nop 0
	v_addc_co_u32_e32 v3, vcc, 0, v163, vcc
	v_add_co_u32_e32 v4, vcc, s0, v162
	s_mov_b32 s0, 0x828000
	s_nop 0
	v_addc_co_u32_e32 v5, vcc, 0, v163, vcc
	global_load_dwordx4 v[18:21], v[2:3], off sc0 nt
	global_load_dwordx4 v[26:29], v[4:5], off sc0 nt
	v_add_co_u32_e32 v2, vcc, s0, v162
	s_mov_b32 s0, 0x82c000
	s_nop 0
	v_addc_co_u32_e32 v3, vcc, 0, v163, vcc
	v_add_co_u32_e32 v4, vcc, s0, v162
	s_mov_b32 s0, 0x830000
	s_nop 0
	v_addc_co_u32_e32 v5, vcc, 0, v163, vcc
	global_load_dwordx4 v[50:53], v[2:3], off sc0 nt
	global_load_dwordx4 v[58:61], v[4:5], off sc0 nt
	v_add_co_u32_e32 v2, vcc, s0, v162
	s_mov_b32 s0, 0x834000
	s_nop 0
	v_addc_co_u32_e32 v3, vcc, 0, v163, vcc
	v_add_co_u32_e32 v6, vcc, s0, v162
	s_mov_b32 s0, 0x838000
	s_nop 0
	v_addc_co_u32_e32 v7, vcc, 0, v163, vcc
	v_add_co_u32_e32 v22, vcc, s0, v162
	s_mov_b32 s0, 0x83c000
	s_nop 0
	v_addc_co_u32_e32 v23, vcc, 0, v163, vcc
	v_add_co_u32_e32 v34, vcc, s0, v162
	global_load_dwordx4 v[2:5], v[2:3], off sc0 nt
	s_nop 0
	global_load_dwordx4 v[6:9], v[6:7], off sc0 nt
	v_addc_co_u32_e32 v35, vcc, 0, v163, vcc
	global_load_dwordx4 v[22:25], v[22:23], off sc0 nt
	s_nop 0
	global_load_dwordx4 v[34:37], v[34:35], off sc0 nt
	v_add_u32_e32 v166, 0, v154
	v_mad_u64_u32 v[142:143], s[0:1], v132, s42, v[166:167]
	ds_read_b128 v[130:133], v142
	v_lshl_add_u64 v[168:169], s[30:31], 0, v[154:155]
	v_lshl_add_u64 v[144:145], v[168:169], 0, v[134:135]
	v_mad_u64_u32 v[146:147], s[0:1], v136, s42, v[166:167]
	s_waitcnt lgkmcnt(0)
	global_store_dwordx4 v[144:145], v[130:133], off nt
	ds_read_b128 v[130:133], v146
	v_lshl_add_u64 v[148:149], v[168:169], 0, v[138:139]
	v_mad_u64_u32 v[150:151], s[0:1], v140, s42, v[166:167]
	v_lshl_add_u64 v[152:153], v[168:169], 0, v[152:153]
	s_waitcnt lgkmcnt(0)
	global_store_dwordx4 v[148:149], v[130:133], off nt
	ds_read_b128 v[130:133], v150
	v_mad_u64_u32 v[158:159], s[0:1], v158, s42, v[166:167]
	v_lshl_add_u64 v[160:161], v[168:169], 0, v[160:161]
	s_waitcnt lgkmcnt(0)
	global_store_dwordx4 v[152:153], v[130:133], off nt
	ds_read_b128 v[130:133], v158
	s_waitcnt lgkmcnt(0)
	global_store_dwordx4 v[160:161], v[130:133], off nt
	s_waitcnt vmcnt(35)
	v_mul_f32_e32 v106, 0x43800000, v106
	s_waitcnt vmcnt(34)
	v_mul_f32_e32 v110, 0x43800000, v110
	s_waitcnt vmcnt(31)
	v_mul_f32_e32 v70, 0x43800000, v70
	s_waitcnt vmcnt(30)
	v_mul_f32_e32 v78, 0x43800000, v78
	s_waitcnt vmcnt(27)
	v_mul_f32_e32 v30, 0x43800000, v30
	s_waitcnt vmcnt(26)
	v_mul_f32_e32 v42, 0x43800000, v42
	s_waitcnt vmcnt(23)
	v_mul_f32_e32 v10, 0x43800000, v10
	s_waitcnt vmcnt(22)
	v_mul_f32_e32 v14, 0x43800000, v14
	v_med3_f32 v106, v106, s85, v252
	v_med3_f32 v110, v110, s85, v252
	v_mov_b32_e32 v130, v155
	v_med3_f32 v70, v70, s85, v252
	v_med3_f32 v78, v78, s85, v252
	v_mov_b32_e32 v131, v155
	v_med3_f32 v30, v30, s85, v252
	v_med3_f32 v42, v42, s85, v252
	v_mov_b32_e32 v132, v155
	v_med3_f32 v10, v10, s85, v252
	v_med3_f32 v14, v14, s85, v252
	v_mov_b32_e32 v133, v155
	v_cvt_pk_fp8_f32 v130, v106, v110
	v_cvt_pk_fp8_f32 v131, v70, v78
	v_cvt_pk_fp8_f32 v132, v30, v42
	v_cvt_pk_fp8_f32 v133, v10, v14
	v_mul_f32_e32 v122, 0x43800000, v122
	v_mul_f32_e32 v126, 0x43800000, v126
	v_mul_f32_e32 v90, 0x43800000, v90
	v_mul_f32_e32 v94, 0x43800000, v94
	v_mul_f32_e32 v62, 0x43800000, v62
	v_mul_f32_e32 v70, 0x43800000, v74
	s_waitcnt vmcnt(21)
	v_mul_f32_e32 v30, 0x43800000, v38
	s_waitcnt vmcnt(20)
	v_mul_f32_e32 v38, 0x43800000, v46
	v_med3_f32 v122, v122, s85, v252
	v_med3_f32 v126, v126, s85, v252
	v_med3_f32 v90, v90, s85, v252
	v_med3_f32 v94, v94, s85, v252
	v_med3_f32 v62, v62, s85, v252
	v_med3_f32 v70, v70, s85, v252
	v_med3_f32 v30, v30, s85, v252
	v_med3_f32 v38, v38, s85, v252
	v_cvt_pk_fp8_f32 v130, v122, v126 op_sel:[0,0,1]
	v_cvt_pk_fp8_f32 v131, v90, v94 op_sel:[0,0,1]
	v_cvt_pk_fp8_f32 v132, v62, v70 op_sel:[0,0,1]
	v_cvt_pk_fp8_f32 v133, v30, v38 op_sel:[0,0,1]
	v_mul_f32_e32 v10, 0x43800000, v107
	v_mul_f32_e32 v14, 0x43800000, v111
	v_med3_f32 v10, v10, s85, v252
	ds_write_b128 v164, v[130:133] offset:34816
	v_med3_f32 v14, v14, s85, v252
	v_mov_b32_e32 v130, v155
	v_cvt_pk_fp8_f32 v130, v10, v14
	v_mul_f32_e32 v10, 0x43800000, v71
	v_mul_f32_e32 v14, 0x43800000, v79
	v_med3_f32 v10, v10, s85, v252
	v_med3_f32 v14, v14, s85, v252
	v_mov_b32_e32 v131, v155
	v_cvt_pk_fp8_f32 v131, v10, v14
	v_mul_f32_e32 v10, 0x43800000, v31
	v_mul_f32_e32 v14, 0x43800000, v43
	v_med3_f32 v10, v10, s85, v252
	v_med3_f32 v14, v14, s85, v252
	v_mov_b32_e32 v132, v155
	v_mul_f32_e32 v30, 0x43800000, v123
	v_mul_f32_e32 v38, 0x43800000, v127
	v_cvt_pk_fp8_f32 v132, v10, v14
	v_mul_f32_e32 v10, 0x43800000, v11
	v_mul_f32_e32 v11, 0x43800000, v15
	v_med3_f32 v30, v30, s85, v252
	v_med3_f32 v38, v38, s85, v252
	v_med3_f32 v10, v10, s85, v252
	v_med3_f32 v11, v11, s85, v252
	v_mov_b32_e32 v133, v155
	v_cvt_pk_fp8_f32 v130, v30, v38 op_sel:[0,0,1]
	v_mul_f32_e32 v30, 0x43800000, v91
	v_mul_f32_e32 v38, 0x43800000, v95
	v_cvt_pk_fp8_f32 v133, v10, v11
	v_med3_f32 v30, v30, s85, v252
	v_med3_f32 v38, v38, s85, v252
	v_cvt_pk_fp8_f32 v131, v30, v38 op_sel:[0,0,1]
	v_mul_f32_e32 v30, 0x43800000, v63
	v_mul_f32_e32 v31, 0x43800000, v75
	v_mul_f32_e32 v14, 0x43800000, v39
	v_mul_f32_e32 v15, 0x43800000, v47
	v_med3_f32 v30, v30, s85, v252
	v_med3_f32 v31, v31, s85, v252
	v_med3_f32 v14, v14, s85, v252
	v_med3_f32 v15, v15, s85, v252
	v_cvt_pk_fp8_f32 v132, v30, v31 op_sel:[0,0,1]
	v_cvt_pk_fp8_f32 v133, v14, v15 op_sel:[0,0,1]
	v_mul_f32_e32 v10, 0x43800000, v108
	v_mul_f32_e32 v11, 0x43800000, v112
	v_med3_f32 v10, v10, s85, v252
	ds_write_b128 v164, v[130:133] offset:35088
	v_med3_f32 v11, v11, s85, v252
	v_mov_b32_e32 v130, v155
	v_cvt_pk_fp8_f32 v130, v10, v11
	v_mul_f32_e32 v10, 0x43800000, v72
	v_mul_f32_e32 v11, 0x43800000, v80
	v_med3_f32 v10, v10, s85, v252
	v_med3_f32 v11, v11, s85, v252
	v_mov_b32_e32 v131, v155
	v_mul_f32_e32 v14, 0x43800000, v124
	v_mul_f32_e32 v15, 0x43800000, v128
	v_cvt_pk_fp8_f32 v131, v10, v11
	v_mul_f32_e32 v10, 0x43800000, v32
	v_mul_f32_e32 v11, 0x43800000, v44
	v_med3_f32 v14, v14, s85, v252
	v_med3_f32 v15, v15, s85, v252
	v_med3_f32 v10, v10, s85, v252
	v_med3_f32 v11, v11, s85, v252
	v_mov_b32_e32 v132, v155
	v_cvt_pk_fp8_f32 v130, v14, v15 op_sel:[0,0,1]
	v_mul_f32_e32 v14, 0x43800000, v92
	v_mul_f32_e32 v15, 0x43800000, v96
	v_cvt_pk_fp8_f32 v132, v10, v11
	v_med3_f32 v14, v14, s85, v252
	v_med3_f32 v15, v15, s85, v252
	v_mul_f32_e32 v10, 0x43800000, v12
	v_mul_f32_e32 v11, 0x43800000, v16
	v_cvt_pk_fp8_f32 v131, v14, v15 op_sel:[0,0,1]
	v_mul_f32_e32 v14, 0x43800000, v64
	v_mul_f32_e32 v15, 0x43800000, v76
	v_med3_f32 v10, v10, s85, v252
	v_med3_f32 v11, v11, s85, v252
	v_mov_b32_e32 v133, v155
	v_med3_f32 v14, v14, s85, v252
	v_med3_f32 v15, v15, s85, v252
	v_cvt_pk_fp8_f32 v133, v10, v11
	v_mul_f32_e32 v10, 0x43800000, v109
	v_mul_f32_e32 v11, 0x43800000, v113
	v_cvt_pk_fp8_f32 v132, v14, v15 op_sel:[0,0,1]
	v_med3_f32 v15, v10, s85, v252
	v_med3_f32 v11, v11, s85, v252
	v_mov_b32_e32 v10, v155
	v_mul_f32_e32 v12, 0x43800000, v40
	v_mul_f32_e32 v14, 0x43800000, v48
	v_cvt_pk_fp8_f32 v10, v15, v11
	v_med3_f32 v12, v12, s85, v252
	v_med3_f32 v14, v14, s85, v252
	v_cvt_pk_fp8_f32 v133, v12, v14 op_sel:[0,0,1]
	v_mul_f32_e32 v12, 0x43800000, v125
	v_mul_f32_e32 v14, 0x43800000, v129
	v_med3_f32 v12, v12, s85, v252
	v_med3_f32 v14, v14, s85, v252
	v_cvt_pk_fp8_f32 v10, v12, v14 op_sel:[0,0,1]
	v_mul_f32_e32 v11, 0x43800000, v73
	v_mul_f32_e32 v12, 0x43800000, v81
	v_med3_f32 v16, v11, s85, v252
	v_med3_f32 v12, v12, s85, v252
	v_mov_b32_e32 v11, v155
	v_cvt_pk_fp8_f32 v11, v16, v12
	v_mul_f32_e32 v14, 0x43800000, v93
	v_mul_f32_e32 v15, 0x43800000, v97
	v_med3_f32 v14, v14, s85, v252
	v_med3_f32 v15, v15, s85, v252
	v_cvt_pk_fp8_f32 v11, v14, v15 op_sel:[0,0,1]
	v_mul_f32_e32 v12, 0x43800000, v33
	v_mul_f32_e32 v14, 0x43800000, v45
	v_med3_f32 v30, v12, s85, v252
	v_med3_f32 v14, v14, s85, v252
	v_mov_b32_e32 v12, v155
	v_cvt_pk_fp8_f32 v12, v30, v14
	v_mul_f32_e32 v13, 0x43800000, v13
	v_mul_f32_e32 v14, 0x43800000, v17
	v_med3_f32 v17, v13, s85, v252
	v_med3_f32 v14, v14, s85, v252
	v_mov_b32_e32 v13, v155
	v_mul_f32_e32 v15, 0x43800000, v65
	v_mul_f32_e32 v16, 0x43800000, v77
	v_cvt_pk_fp8_f32 v13, v17, v14
	v_med3_f32 v15, v15, s85, v252
	v_med3_f32 v16, v16, s85, v252
	v_cvt_pk_fp8_f32 v12, v15, v16 op_sel:[0,0,1]
	v_mul_f32_e32 v15, 0x43800000, v41
	v_mul_f32_e32 v16, 0x43800000, v49
	v_med3_f32 v15, v15, s85, v252
	v_med3_f32 v16, v16, s85, v252
	v_cvt_pk_fp8_f32 v13, v15, v16 op_sel:[0,0,1]
	ds_write_b128 v164, v[130:133] offset:35360
	ds_write_b128 v164, v[10:13] offset:35632
	s_waitcnt lgkmcnt(0)
	s_barrier
	v_add_co_u32_e32 v10, vcc, s73, v162
	s_mov_b32 s0, 0xc20000
	s_nop 0
	v_addc_co_u32_e32 v11, vcc, 0, v163, vcc
	v_add_co_u32_e32 v12, vcc, s75, v162
	s_nop 1
	v_addc_co_u32_e32 v13, vcc, 0, v163, vcc
	global_load_dwordx4 v[122:125], v[10:11], off sc0 nt
	global_load_dwordx4 v[126:129], v[12:13], off sc0 nt
	v_add_co_u32_e32 v10, vcc, s76, v162
	s_nop 1
	v_addc_co_u32_e32 v11, vcc, 0, v163, vcc
	v_add_co_u32_e32 v12, vcc, s82, v162
	s_nop 1
	v_addc_co_u32_e32 v13, vcc, 0, v163, vcc
	global_load_dwordx4 v[134:137], v[10:11], off sc0 nt
	global_load_dwordx4 v[138:141], v[12:13], off sc0 nt
	v_add_co_u32_e32 v10, vcc, s89, v162
	s_nop 1
	v_addc_co_u32_e32 v11, vcc, 0, v163, vcc
	v_add_co_u32_e32 v12, vcc, s91, v162
	s_nop 1
	v_addc_co_u32_e32 v13, vcc, 0, v163, vcc
	global_load_dwordx4 v[74:77], v[10:11], off sc0 nt
	global_load_dwordx4 v[94:97], v[12:13], off sc0 nt
	v_add_co_u32_e32 v10, vcc, s92, v162
	s_nop 1
	v_addc_co_u32_e32 v11, vcc, 0, v163, vcc
	v_add_co_u32_e32 v12, vcc, s93, v162
	s_nop 1
	v_addc_co_u32_e32 v13, vcc, 0, v163, vcc
	global_load_dwordx4 v[106:109], v[10:11], off sc0 nt
	global_load_dwordx4 v[110:113], v[12:13], off sc0 nt
	v_add_co_u32_e32 v10, vcc, s0, v162
	s_mov_b32 s0, 0xc24000
	s_nop 0
	v_addc_co_u32_e32 v11, vcc, 0, v163, vcc
	v_add_co_u32_e32 v12, vcc, s0, v162
	s_mov_b32 s0, 0xc28000
	s_nop 0
	v_addc_co_u32_e32 v13, vcc, 0, v163, vcc
	global_load_dwordx4 v[30:33], v[10:11], off sc0 nt
	global_load_dwordx4 v[42:45], v[12:13], off sc0 nt
	v_add_co_u32_e32 v10, vcc, s0, v162
	s_mov_b32 s0, 0xc2c000
	s_nop 0
	v_addc_co_u32_e32 v11, vcc, 0, v163, vcc
	v_add_co_u32_e32 v12, vcc, s0, v162
	s_mov_b32 s0, 0xc30000
	s_nop 0
	v_addc_co_u32_e32 v13, vcc, 0, v163, vcc
	global_load_dwordx4 v[70:73], v[10:11], off sc0 nt
	global_load_dwordx4 v[90:93], v[12:13], off sc0 nt
	v_add_co_u32_e32 v10, vcc, s0, v162
	s_mov_b32 s0, 0xc34000
	s_nop 0
	v_addc_co_u32_e32 v11, vcc, 0, v163, vcc
	v_add_co_u32_e32 v14, vcc, s0, v162
	s_mov_b32 s0, 0xc38000
	s_nop 0
	v_addc_co_u32_e32 v15, vcc, 0, v163, vcc
	v_add_co_u32_e32 v38, vcc, s0, v162
	s_mov_b32 s0, 0xc3c000
	s_nop 0
	v_addc_co_u32_e32 v39, vcc, 0, v163, vcc
	v_add_co_u32_e32 v46, vcc, s0, v162
	global_load_dwordx4 v[10:13], v[10:11], off sc0 nt
	s_nop 0
	global_load_dwordx4 v[14:17], v[14:15], off sc0 nt
	v_addc_co_u32_e32 v47, vcc, 0, v163, vcc
	global_load_dwordx4 v[38:41], v[38:39], off sc0 nt
	s_nop 0
	global_load_dwordx4 v[62:65], v[46:47], off sc0 nt
	ds_read_b128 v[46:49], v142 offset:34816
	s_waitcnt lgkmcnt(0)
	global_store_dwordx4 v[144:145], v[46:49], off offset:256 nt
	ds_read_b128 v[46:49], v146 offset:34816
	s_waitcnt lgkmcnt(0)
	global_store_dwordx4 v[148:149], v[46:49], off offset:256 nt
	ds_read_b128 v[46:49], v150 offset:34816
	s_waitcnt lgkmcnt(0)
	global_store_dwordx4 v[152:153], v[46:49], off offset:256 nt
	ds_read_b128 v[46:49], v158 offset:34816
	s_waitcnt lgkmcnt(0)
	global_store_dwordx4 v[160:161], v[46:49], off offset:256 nt
	s_waitcnt vmcnt(39)
	s_nop 0
	v_mul_f32_e32 v46, 0x43800000, v98
	s_waitcnt vmcnt(38)
	v_mul_f32_e32 v47, 0x43800000, v102
	v_med3_f32 v78, v46, s85, v252
	v_med3_f32 v47, v47, s85, v252
	v_mov_b32_e32 v46, v155
	v_cvt_pk_fp8_f32 v46, v78, v47
	s_waitcnt vmcnt(37)
	v_mul_f32_e32 v48, 0x43800000, v114
	s_waitcnt vmcnt(36)
	v_mul_f32_e32 v49, 0x43800000, v118
	v_med3_f32 v48, v48, s85, v252
	v_med3_f32 v49, v49, s85, v252
	v_cvt_pk_fp8_f32 v46, v48, v49 op_sel:[0,0,1]
	s_waitcnt vmcnt(35)
	v_mul_f32_e32 v47, 0x43800000, v54
	s_waitcnt vmcnt(34)
	v_mul_f32_e32 v48, 0x43800000, v66
	v_med3_f32 v66, v47, s85, v252
	v_med3_f32 v48, v48, s85, v252
	v_mov_b32_e32 v47, v155
	v_cvt_pk_fp8_f32 v47, v66, v48
	s_waitcnt vmcnt(31)
	v_mul_f32_e32 v18, 0x43800000, v18
	s_waitcnt vmcnt(30)
	v_mul_f32_e32 v26, 0x43800000, v26
	s_waitcnt vmcnt(29)
	v_mul_f32_e32 v48, 0x43800000, v50
	v_med3_f32 v18, v18, s85, v252
	v_med3_f32 v26, v26, s85, v252
	v_med3_f32 v50, v48, s85, v252
	v_mov_b32_e32 v48, v155
	v_mul_f32_e32 v49, 0x43800000, v82
	v_mul_f32_e32 v54, 0x43800000, v86
	v_cvt_pk_fp8_f32 v48, v18, v26
	v_med3_f32 v49, v49, s85, v252
	v_med3_f32 v54, v54, s85, v252
	v_cvt_pk_fp8_f32 v47, v49, v54 op_sel:[0,0,1]
	s_waitcnt vmcnt(28)
	v_mul_f32_e32 v49, 0x43800000, v58
	v_med3_f32 v49, v49, s85, v252
	s_waitcnt vmcnt(27)
	v_mul_f32_e32 v2, 0x43800000, v2
	s_waitcnt vmcnt(26)
	v_mul_f32_e32 v6, 0x43800000, v6
	v_cvt_pk_fp8_f32 v48, v50, v49 op_sel:[0,0,1]
	v_med3_f32 v2, v2, s85, v252
	v_med3_f32 v6, v6, s85, v252
	v_mov_b32_e32 v49, v155
	v_cvt_pk_fp8_f32 v49, v2, v6
	s_waitcnt vmcnt(25)
	v_mul_f32_e32 v18, 0x43800000, v22
	s_waitcnt vmcnt(24)
	v_mul_f32_e32 v22, 0x43800000, v34
	v_med3_f32 v18, v18, s85, v252
	v_med3_f32 v22, v22, s85, v252
	v_cvt_pk_fp8_f32 v49, v18, v22 op_sel:[0,0,1]
	v_mul_f32_e32 v2, 0x43800000, v99
	v_mul_f32_e32 v6, 0x43800000, v103
	v_med3_f32 v2, v2, s85, v252
	ds_write_b128 v164, v[46:49]
	v_med3_f32 v6, v6, s85, v252
	v_mov_b32_e32 v46, v155
	v_cvt_pk_fp8_f32 v46, v2, v6
	v_mul_f32_e32 v2, 0x43800000, v55
	v_mul_f32_e32 v6, 0x43800000, v67
	v_med3_f32 v2, v2, s85, v252
	v_med3_f32 v6, v6, s85, v252
	v_mov_b32_e32 v47, v155
	v_cvt_pk_fp8_f32 v47, v2, v6
	v_mul_f32_e32 v2, 0x43800000, v19
	v_mul_f32_e32 v6, 0x43800000, v27
	v_med3_f32 v2, v2, s85, v252
	v_med3_f32 v6, v6, s85, v252
	v_mov_b32_e32 v48, v155
	v_mul_f32_e32 v18, 0x43800000, v115
	v_mul_f32_e32 v22, 0x43800000, v119
	v_cvt_pk_fp8_f32 v48, v2, v6
	v_mul_f32_e32 v2, 0x43800000, v3
	v_mul_f32_e32 v3, 0x43800000, v7
	v_med3_f32 v18, v18, s85, v252
	v_med3_f32 v22, v22, s85, v252
	v_med3_f32 v2, v2, s85, v252
	v_med3_f32 v3, v3, s85, v252
	v_mov_b32_e32 v49, v155
	v_cvt_pk_fp8_f32 v46, v18, v22 op_sel:[0,0,1]
	v_mul_f32_e32 v18, 0x43800000, v83
	v_mul_f32_e32 v22, 0x43800000, v87
	v_cvt_pk_fp8_f32 v49, v2, v3
	v_med3_f32 v18, v18, s85, v252
	v_med3_f32 v22, v22, s85, v252
	v_cvt_pk_fp8_f32 v47, v18, v22 op_sel:[0,0,1]
	v_mul_f32_e32 v18, 0x43800000, v51
	v_mul_f32_e32 v19, 0x43800000, v59
	v_mul_f32_e32 v6, 0x43800000, v23
	v_mul_f32_e32 v7, 0x43800000, v35
	v_med3_f32 v18, v18, s85, v252
	v_med3_f32 v19, v19, s85, v252
	v_med3_f32 v6, v6, s85, v252
	v_med3_f32 v7, v7, s85, v252
	v_cvt_pk_fp8_f32 v48, v18, v19 op_sel:[0,0,1]
	v_cvt_pk_fp8_f32 v49, v6, v7 op_sel:[0,0,1]
	v_mul_f32_e32 v2, 0x43800000, v100
	v_mul_f32_e32 v3, 0x43800000, v104
	v_med3_f32 v2, v2, s85, v252
	ds_write_b128 v164, v[46:49] offset:272
	v_med3_f32 v3, v3, s85, v252
	v_mov_b32_e32 v46, v155
	v_cvt_pk_fp8_f32 v46, v2, v3
	v_mul_f32_e32 v2, 0x43800000, v56
	v_mul_f32_e32 v3, 0x43800000, v68
	v_med3_f32 v2, v2, s85, v252
	v_med3_f32 v3, v3, s85, v252
	v_mov_b32_e32 v47, v155
	v_mul_f32_e32 v6, 0x43800000, v116
	v_mul_f32_e32 v7, 0x43800000, v120
	v_cvt_pk_fp8_f32 v47, v2, v3
	v_mul_f32_e32 v2, 0x43800000, v20
	v_mul_f32_e32 v3, 0x43800000, v28
	v_med3_f32 v6, v6, s85, v252
	v_med3_f32 v7, v7, s85, v252
	v_med3_f32 v2, v2, s85, v252
	v_med3_f32 v3, v3, s85, v252
	v_mov_b32_e32 v48, v155
	v_cvt_pk_fp8_f32 v46, v6, v7 op_sel:[0,0,1]
	v_mul_f32_e32 v6, 0x43800000, v84
	v_mul_f32_e32 v7, 0x43800000, v88
	v_cvt_pk_fp8_f32 v48, v2, v3
	v_med3_f32 v6, v6, s85, v252
	v_med3_f32 v7, v7, s85, v252
	v_mul_f32_e32 v2, 0x43800000, v4
	v_mul_f32_e32 v3, 0x43800000, v8
	v_cvt_pk_fp8_f32 v47, v6, v7 op_sel:[0,0,1]
	v_mul_f32_e32 v6, 0x43800000, v52
	v_mul_f32_e32 v7, 0x43800000, v60
	v_med3_f32 v2, v2, s85, v252
	v_med3_f32 v3, v3, s85, v252
	v_mov_b32_e32 v49, v155
	v_med3_f32 v6, v6, s85, v252
	v_med3_f32 v7, v7, s85, v252
	v_cvt_pk_fp8_f32 v49, v2, v3
	v_mul_f32_e32 v2, 0x43800000, v101
	v_mul_f32_e32 v3, 0x43800000, v105
	v_cvt_pk_fp8_f32 v48, v6, v7 op_sel:[0,0,1]
	v_med3_f32 v7, v2, s85, v252
	v_med3_f32 v3, v3, s85, v252
	v_mov_b32_e32 v2, v155
	v_mul_f32_e32 v4, 0x43800000, v24
	v_mul_f32_e32 v6, 0x43800000, v36
	v_cvt_pk_fp8_f32 v2, v7, v3
	v_med3_f32 v4, v4, s85, v252
	v_med3_f32 v6, v6, s85, v252
	v_cvt_pk_fp8_f32 v49, v4, v6 op_sel:[0,0,1]
	v_mul_f32_e32 v4, 0x43800000, v117
	v_mul_f32_e32 v6, 0x43800000, v121
	v_med3_f32 v4, v4, s85, v252
	v_med3_f32 v6, v6, s85, v252
	v_cvt_pk_fp8_f32 v2, v4, v6 op_sel:[0,0,1]
	v_mul_f32_e32 v3, 0x43800000, v57
	v_mul_f32_e32 v4, 0x43800000, v69
	v_med3_f32 v8, v3, s85, v252
	v_med3_f32 v4, v4, s85, v252
	v_mov_b32_e32 v3, v155
	v_cvt_pk_fp8_f32 v3, v8, v4
	v_mul_f32_e32 v6, 0x43800000, v85
	v_mul_f32_e32 v7, 0x43800000, v89
	v_med3_f32 v6, v6, s85, v252
	v_med3_f32 v7, v7, s85, v252
	v_cvt_pk_fp8_f32 v3, v6, v7 op_sel:[0,0,1]
	v_mul_f32_e32 v4, 0x43800000, v21
	v_mul_f32_e32 v6, 0x43800000, v29
	v_med3_f32 v18, v4, s85, v252
	v_med3_f32 v6, v6, s85, v252
	v_mov_b32_e32 v4, v155
	v_cvt_pk_fp8_f32 v4, v18, v6
	v_mul_f32_e32 v5, 0x43800000, v5
	v_mul_f32_e32 v6, 0x43800000, v9
	v_med3_f32 v9, v5, s85, v252
	v_med3_f32 v6, v6, s85, v252
	v_mov_b32_e32 v5, v155
	v_mul_f32_e32 v7, 0x43800000, v53
	v_mul_f32_e32 v8, 0x43800000, v61
	v_cvt_pk_fp8_f32 v5, v9, v6
	v_med3_f32 v7, v7, s85, v252
	v_med3_f32 v8, v8, s85, v252
	v_cvt_pk_fp8_f32 v4, v7, v8 op_sel:[0,0,1]
	v_mul_f32_e32 v7, 0x43800000, v25
	v_mul_f32_e32 v8, 0x43800000, v37
	v_med3_f32 v7, v7, s85, v252
	v_med3_f32 v8, v8, s85, v252
	v_cvt_pk_fp8_f32 v5, v7, v8 op_sel:[0,0,1]
	ds_write_b128 v164, v[46:49] offset:544
	ds_write_b128 v164, v[2:5] offset:816
	s_waitcnt lgkmcnt(0)
	s_barrier
	s_mov_b32 s0, 0x1000000
	v_add_co_u32_e32 v2, vcc, s0, v162
	s_mov_b32 s0, 0x1004000
	s_nop 0
	v_addc_co_u32_e32 v3, vcc, 0, v163, vcc
	v_add_co_u32_e32 v4, vcc, s0, v162
	s_mov_b32 s0, 0x1008000
	s_nop 0
	v_addc_co_u32_e32 v5, vcc, 0, v163, vcc
	global_load_dwordx4 v[86:89], v[2:3], off sc0 nt
	global_load_dwordx4 v[102:105], v[4:5], off sc0 nt
	v_add_co_u32_e32 v2, vcc, s0, v162
	s_mov_b32 s0, 0x100c000
	s_nop 0
	v_addc_co_u32_e32 v3, vcc, 0, v163, vcc
	v_add_co_u32_e32 v4, vcc, s0, v162
	s_mov_b32 s0, 0x1010000
	s_nop 0
	v_addc_co_u32_e32 v5, vcc, 0, v163, vcc
	global_load_dwordx4 v[118:121], v[2:3], off sc0 nt
	global_load_dwordx4 v[130:133], v[4:5], off sc0 nt
	v_add_co_u32_e32 v2, vcc, s0, v162
	s_mov_b32 s0, 0x1014000
	s_nop 0
	v_addc_co_u32_e32 v3, vcc, 0, v163, vcc
	v_add_co_u32_e32 v4, vcc, s0, v162
	s_mov_b32 s0, 0x1018000
	s_nop 0
	v_addc_co_u32_e32 v5, vcc, 0, v163, vcc
	global_load_dwordx4 v[54:57], v[2:3], off sc0 nt
	global_load_dwordx4 v[78:81], v[4:5], off sc0 nt
	v_add_co_u32_e32 v2, vcc, s0, v162
	s_mov_b32 s0, 0x101c000
	s_nop 0
	v_addc_co_u32_e32 v3, vcc, 0, v163, vcc
	v_add_co_u32_e32 v4, vcc, s0, v162
	s_mov_b32 s0, 0x1020000
	s_nop 0
	v_addc_co_u32_e32 v5, vcc, 0, v163, vcc
	global_load_dwordx4 v[98:101], v[2:3], off sc0 nt
	global_load_dwordx4 v[114:117], v[4:5], off sc0 nt
	v_add_co_u32_e32 v2, vcc, s0, v162
	s_mov_b32 s0, 0x1024000
	s_nop 0
	v_addc_co_u32_e32 v3, vcc, 0, v163, vcc
	v_add_co_u32_e32 v4, vcc, s0, v162
	s_mov_b32 s0, 0x1028000
	s_nop 0
	v_addc_co_u32_e32 v5, vcc, 0, v163, vcc
	global_load_dwordx4 v[22:25], v[2:3], off sc0 nt
	global_load_dwordx4 v[46:49], v[4:5], off sc0 nt
	v_add_co_u32_e32 v2, vcc, s0, v162
	s_mov_b32 s0, 0x102c000
	s_nop 0
	v_addc_co_u32_e32 v3, vcc, 0, v163, vcc
	v_add_co_u32_e32 v4, vcc, s0, v162
	s_mov_b32 s0, 0x1030000
	s_nop 0
	v_addc_co_u32_e32 v5, vcc, 0, v163, vcc
	global_load_dwordx4 v[66:69], v[2:3], off sc0 nt
	global_load_dwordx4 v[82:85], v[4:5], off sc0 nt
	v_add_co_u32_e32 v2, vcc, s0, v162
	s_mov_b32 s0, 0x1034000
	s_nop 0
	v_addc_co_u32_e32 v3, vcc, 0, v163, vcc
	v_add_co_u32_e32 v6, vcc, s0, v162
	s_mov_b32 s0, 0x1038000
	s_nop 0
	v_addc_co_u32_e32 v7, vcc, 0, v163, vcc
	global_load_dwordx4 v[2:5], v[2:3], off sc0 nt
	s_nop 0
	global_load_dwordx4 v[18:21], v[6:7], off sc0 nt
	v_add_co_u32_e32 v6, vcc, s0, v162
	s_mov_b32 s0, 0x103c000
	s_nop 0
	v_addc_co_u32_e32 v7, vcc, 0, v163, vcc
	v_add_co_u32_e32 v8, vcc, s0, v162
	s_nop 1
	v_addc_co_u32_e32 v9, vcc, 0, v163, vcc
	global_load_dwordx4 v[34:37], v[6:7], off sc0 nt
	global_load_dwordx4 v[50:53], v[8:9], off sc0 nt
	ds_read_b128 v[6:9], v142
	s_waitcnt lgkmcnt(0)
	global_store_dwordx4 v[144:145], v[6:9], off offset:512 nt
	ds_read_b128 v[6:9], v146
	s_waitcnt lgkmcnt(0)
	global_store_dwordx4 v[148:149], v[6:9], off offset:512 nt
	ds_read_b128 v[6:9], v150
	s_waitcnt lgkmcnt(0)
	global_store_dwordx4 v[152:153], v[6:9], off offset:512 nt
	ds_read_b128 v[6:9], v158
	s_waitcnt lgkmcnt(0)
	global_store_dwordx4 v[160:161], v[6:9], off offset:512 nt
	s_waitcnt vmcnt(39)
	s_nop 0
	v_mul_f32_e32 v6, 0x43800000, v122
	s_waitcnt vmcnt(38)
	v_mul_f32_e32 v7, 0x43800000, v126
	v_med3_f32 v26, v6, s85, v252
	v_med3_f32 v7, v7, s85, v252
	v_mov_b32_e32 v6, v155
	v_cvt_pk_fp8_f32 v6, v26, v7
	s_waitcnt vmcnt(37)
	v_mul_f32_e32 v8, 0x43800000, v134
	s_waitcnt vmcnt(36)
	v_mul_f32_e32 v9, 0x43800000, v138
	v_med3_f32 v8, v8, s85, v252
	v_med3_f32 v9, v9, s85, v252
	v_cvt_pk_fp8_f32 v6, v8, v9 op_sel:[0,0,1]
	s_waitcnt vmcnt(35)
	v_mul_f32_e32 v7, 0x43800000, v74
	s_waitcnt vmcnt(34)
	v_mul_f32_e32 v8, 0x43800000, v94
	v_med3_f32 v27, v7, s85, v252
	v_med3_f32 v8, v8, s85, v252
	v_mov_b32_e32 v7, v155
	v_cvt_pk_fp8_f32 v7, v27, v8
	s_waitcnt vmcnt(33)
	v_mul_f32_e32 v9, 0x43800000, v106
	s_waitcnt vmcnt(32)
	v_mul_f32_e32 v26, 0x43800000, v110
	v_med3_f32 v9, v9, s85, v252
	v_med3_f32 v26, v26, s85, v252
	v_cvt_pk_fp8_f32 v7, v9, v26 op_sel:[0,0,1]
	s_waitcnt vmcnt(31)
	v_mul_f32_e32 v8, 0x43800000, v30
	s_waitcnt vmcnt(30)
	v_mul_f32_e32 v9, 0x43800000, v42
	v_med3_f32 v28, v8, s85, v252
	v_med3_f32 v9, v9, s85, v252
	v_mov_b32_e32 v8, v155
	v_cvt_pk_fp8_f32 v8, v28, v9
	s_waitcnt vmcnt(29)
	v_mul_f32_e32 v26, 0x43800000, v70
	s_waitcnt vmcnt(28)
	v_mul_f32_e32 v27, 0x43800000, v90
	v_med3_f32 v26, v26, s85, v252
	v_med3_f32 v27, v27, s85, v252
	s_waitcnt vmcnt(27)
	v_mul_f32_e32 v9, 0x43800000, v10
	s_waitcnt vmcnt(26)
	v_mul_f32_e32 v10, 0x43800000, v14
	v_cvt_pk_fp8_f32 v8, v26, v27 op_sel:[0,0,1]
	v_med3_f32 v27, v9, s85, v252
	v_med3_f32 v10, v10, s85, v252
	v_mov_b32_e32 v9, v155
	v_cvt_pk_fp8_f32 v9, v27, v10
	s_waitcnt vmcnt(25)
	v_mul_f32_e32 v14, 0x43800000, v38
	s_waitcnt vmcnt(24)
	v_mul_f32_e32 v26, 0x43800000, v62
	v_med3_f32 v14, v14, s85, v252
	v_med3_f32 v26, v26, s85, v252
	v_cvt_pk_fp8_f32 v9, v14, v26 op_sel:[0,0,1]
	ds_write_b128 v164, v[6:9] offset:34816
	v_mul_f32_e32 v6, 0x43800000, v123
	v_mul_f32_e32 v7, 0x43800000, v127
	v_med3_f32 v10, v6, s85, v252
	v_med3_f32 v7, v7, s85, v252
	v_mov_b32_e32 v6, v155
	v_cvt_pk_fp8_f32 v6, v10, v7
	v_mul_f32_e32 v8, 0x43800000, v135
	v_mul_f32_e32 v9, 0x43800000, v139
	v_med3_f32 v8, v8, s85, v252
	v_med3_f32 v9, v9, s85, v252
	v_cvt_pk_fp8_f32 v6, v8, v9 op_sel:[0,0,1]
	v_mul_f32_e32 v7, 0x43800000, v75
	v_mul_f32_e32 v8, 0x43800000, v95
	v_med3_f32 v14, v7, s85, v252
	v_med3_f32 v8, v8, s85, v252
	v_mov_b32_e32 v7, v155
	v_cvt_pk_fp8_f32 v7, v14, v8
	v_mul_f32_e32 v9, 0x43800000, v107
	v_mul_f32_e32 v10, 0x43800000, v111
	v_med3_f32 v9, v9, s85, v252
	v_med3_f32 v10, v10, s85, v252
	v_cvt_pk_fp8_f32 v7, v9, v10 op_sel:[0,0,1]
	v_mul_f32_e32 v8, 0x43800000, v31
	v_mul_f32_e32 v9, 0x43800000, v43
	v_med3_f32 v26, v8, s85, v252
	v_med3_f32 v9, v9, s85, v252
	v_mov_b32_e32 v8, v155
	v_cvt_pk_fp8_f32 v8, v26, v9
	v_mul_f32_e32 v10, 0x43800000, v71
	v_mul_f32_e32 v14, 0x43800000, v91
	v_med3_f32 v10, v10, s85, v252
	v_med3_f32 v14, v14, s85, v252
	v_cvt_pk_fp8_f32 v8, v10, v14 op_sel:[0,0,1]
	v_mul_f32_e32 v9, 0x43800000, v11
	v_mul_f32_e32 v10, 0x43800000, v15
	v_med3_f32 v15, v9, s85, v252
	v_med3_f32 v10, v10, s85, v252
	v_mov_b32_e32 v9, v155
	v_cvt_pk_fp8_f32 v9, v15, v10
	v_mul_f32_e32 v11, 0x43800000, v39
	v_mul_f32_e32 v14, 0x43800000, v63
	v_med3_f32 v11, v11, s85, v252
	v_med3_f32 v14, v14, s85, v252
	v_cvt_pk_fp8_f32 v9, v11, v14 op_sel:[0,0,1]
	ds_write_b128 v164, v[6:9] offset:35088
	v_mul_f32_e32 v6, 0x43800000, v124
	v_mul_f32_e32 v7, 0x43800000, v128
	v_med3_f32 v10, v6, s85, v252
	v_med3_f32 v7, v7, s85, v252
	v_mov_b32_e32 v6, v155
	v_cvt_pk_fp8_f32 v6, v10, v7
	v_mul_f32_e32 v8, 0x43800000, v136
	v_mul_f32_e32 v9, 0x43800000, v140
	v_med3_f32 v8, v8, s85, v252
	v_med3_f32 v9, v9, s85, v252
	v_cvt_pk_fp8_f32 v6, v8, v9 op_sel:[0,0,1]
	v_mul_f32_e32 v7, 0x43800000, v76
	v_mul_f32_e32 v8, 0x43800000, v96
	v_med3_f32 v11, v7, s85, v252
	v_med3_f32 v8, v8, s85, v252
	v_mov_b32_e32 v7, v155
	v_cvt_pk_fp8_f32 v7, v11, v8
	v_mul_f32_e32 v9, 0x43800000, v108
	v_mul_f32_e32 v10, 0x43800000, v112
	v_med3_f32 v9, v9, s85, v252
	v_med3_f32 v10, v10, s85, v252
	v_cvt_pk_fp8_f32 v7, v9, v10 op_sel:[0,0,1]
	v_mul_f32_e32 v8, 0x43800000, v32
	v_mul_f32_e32 v9, 0x43800000, v44
	v_med3_f32 v14, v8, s85, v252
	v_med3_f32 v9, v9, s85, v252
	v_mov_b32_e32 v8, v155
	v_cvt_pk_fp8_f32 v8, v14, v9
	v_mul_f32_e32 v10, 0x43800000, v72
	v_mul_f32_e32 v11, 0x43800000, v92
	v_med3_f32 v10, v10, s85, v252
	v_med3_f32 v11, v11, s85, v252
	v_cvt_pk_fp8_f32 v8, v10, v11 op_sel:[0,0,1]
	v_mul_f32_e32 v9, 0x43800000, v12
	v_mul_f32_e32 v10, 0x43800000, v16
	v_med3_f32 v14, v9, s85, v252
	v_med3_f32 v10, v10, s85, v252
	v_mov_b32_e32 v9, v155
	v_cvt_pk_fp8_f32 v9, v14, v10
	v_mul_f32_e32 v11, 0x43800000, v40
	v_mul_f32_e32 v12, 0x43800000, v64
	v_med3_f32 v11, v11, s85, v252
	v_med3_f32 v12, v12, s85, v252
	v_cvt_pk_fp8_f32 v9, v11, v12 op_sel:[0,0,1]
	ds_write_b128 v164, v[6:9] offset:35360
	v_mul_f32_e32 v6, 0x43800000, v125
	v_mul_f32_e32 v7, 0x43800000, v129
	v_med3_f32 v10, v6, s85, v252
	v_med3_f32 v7, v7, s85, v252
	v_mov_b32_e32 v6, v155
	v_cvt_pk_fp8_f32 v6, v10, v7
	v_mul_f32_e32 v8, 0x43800000, v137
	v_mul_f32_e32 v9, 0x43800000, v141
	v_med3_f32 v8, v8, s85, v252
	v_med3_f32 v9, v9, s85, v252
	v_cvt_pk_fp8_f32 v6, v8, v9 op_sel:[0,0,1]
	v_mul_f32_e32 v7, 0x43800000, v77
	v_mul_f32_e32 v8, 0x43800000, v97
	v_med3_f32 v11, v7, s85, v252
	v_med3_f32 v8, v8, s85, v252
	v_mov_b32_e32 v7, v155
	v_cvt_pk_fp8_f32 v7, v11, v8
	v_mul_f32_e32 v9, 0x43800000, v109
	v_mul_f32_e32 v10, 0x43800000, v113
	v_med3_f32 v9, v9, s85, v252
	v_med3_f32 v10, v10, s85, v252
	v_cvt_pk_fp8_f32 v7, v9, v10 op_sel:[0,0,1]
	v_mul_f32_e32 v8, 0x43800000, v33
	v_mul_f32_e32 v9, 0x43800000, v45
	v_med3_f32 v12, v8, s85, v252
	v_med3_f32 v9, v9, s85, v252
	v_mov_b32_e32 v8, v155
	v_cvt_pk_fp8_f32 v8, v12, v9
	v_mul_f32_e32 v10, 0x43800000, v73
	v_mul_f32_e32 v11, 0x43800000, v93
	v_med3_f32 v10, v10, s85, v252
	v_med3_f32 v11, v11, s85, v252
	v_cvt_pk_fp8_f32 v8, v10, v11 op_sel:[0,0,1]
	v_mul_f32_e32 v9, 0x43800000, v13
	v_mul_f32_e32 v10, 0x43800000, v17
	v_med3_f32 v13, v9, s85, v252
	v_med3_f32 v10, v10, s85, v252
	v_mov_b32_e32 v9, v155
	v_cvt_pk_fp8_f32 v9, v13, v10
	v_mul_f32_e32 v11, 0x43800000, v41
	v_mul_f32_e32 v12, 0x43800000, v65
	v_med3_f32 v11, v11, s85, v252
	v_med3_f32 v12, v12, s85, v252
	v_cvt_pk_fp8_f32 v9, v11, v12 op_sel:[0,0,1]
	ds_write_b128 v164, v[6:9] offset:35632
	s_waitcnt lgkmcnt(0)
	s_barrier
	s_mov_b32 s0, 0x1400000
	v_add_co_u32_e32 v6, vcc, s0, v162
	s_mov_b32 s0, 0x1404000
	s_nop 0
	v_addc_co_u32_e32 v7, vcc, 0, v163, vcc
	v_add_co_u32_e32 v8, vcc, s0, v162
	s_mov_b32 s0, 0x1408000
	s_nop 0
	v_addc_co_u32_e32 v9, vcc, 0, v163, vcc
	global_load_dwordx4 v[90:93], v[6:7], off sc0 nt
	global_load_dwordx4 v[106:109], v[8:9], off sc0 nt
	v_add_co_u32_e32 v6, vcc, s0, v162
	s_mov_b32 s0, 0x140c000
	s_nop 0
	v_addc_co_u32_e32 v7, vcc, 0, v163, vcc
	v_add_co_u32_e32 v8, vcc, s0, v162
	s_mov_b32 s0, 0x1410000
	s_nop 0
	v_addc_co_u32_e32 v9, vcc, 0, v163, vcc
	global_load_dwordx4 v[122:125], v[6:7], off sc0 nt
	global_load_dwordx4 v[126:129], v[8:9], off sc0 nt
	v_add_co_u32_e32 v6, vcc, s0, v162
	s_mov_b32 s0, 0x1414000
	s_nop 0
	v_addc_co_u32_e32 v7, vcc, 0, v163, vcc
	v_add_co_u32_e32 v8, vcc, s0, v162
	s_mov_b32 s0, 0x1418000
	s_nop 0
	v_addc_co_u32_e32 v9, vcc, 0, v163, vcc
	global_load_dwordx4 v[58:61], v[6:7], off sc0 nt
	global_load_dwordx4 v[70:73], v[8:9], off sc0 nt
	v_add_co_u32_e32 v6, vcc, s0, v162
	s_mov_b32 s0, 0x141c000
	s_nop 0
	v_addc_co_u32_e32 v7, vcc, 0, v163, vcc
	v_add_co_u32_e32 v8, vcc, s0, v162
	s_mov_b32 s0, 0x1420000
	s_nop 0
	v_addc_co_u32_e32 v9, vcc, 0, v163, vcc
	global_load_dwordx4 v[94:97], v[6:7], off sc0 nt
	global_load_dwordx4 v[110:113], v[8:9], off sc0 nt
	v_add_co_u32_e32 v6, vcc, s0, v162
	s_mov_b32 s0, 0x1424000
	s_nop 0
	v_addc_co_u32_e32 v7, vcc, 0, v163, vcc
	v_add_co_u32_e32 v8, vcc, s0, v162
	s_mov_b32 s0, 0x1428000
	s_nop 0
	v_addc_co_u32_e32 v9, vcc, 0, v163, vcc
	global_load_dwordx4 v[26:29], v[6:7], off sc0 nt
	global_load_dwordx4 v[38:41], v[8:9], off sc0 nt
	v_add_co_u32_e32 v6, vcc, s0, v162
	s_mov_b32 s0, 0x142c000
	s_nop 0
	v_addc_co_u32_e32 v7, vcc, 0, v163, vcc
	v_add_co_u32_e32 v8, vcc, s0, v162
	s_mov_b32 s0, 0x1430000
	s_nop 0
	v_addc_co_u32_e32 v9, vcc, 0, v163, vcc
	global_load_dwordx4 v[62:65], v[6:7], off sc0 nt
	global_load_dwordx4 v[74:77], v[8:9], off sc0 nt
	v_add_co_u32_e32 v6, vcc, s0, v162
	s_mov_b32 s0, 0x1434000
	s_nop 0
	v_addc_co_u32_e32 v7, vcc, 0, v163, vcc
	v_add_co_u32_e32 v10, vcc, s0, v162
	s_mov_b32 s0, 0x1438000
	s_nop 0
	v_addc_co_u32_e32 v11, vcc, 0, v163, vcc
	v_add_co_u32_e32 v14, vcc, s0, v162
	s_mov_b32 s0, 0x143c000
	s_nop 0
	v_addc_co_u32_e32 v15, vcc, 0, v163, vcc
	v_add_co_u32_e32 v16, vcc, s0, v162
	global_load_dwordx4 v[6:9], v[6:7], off sc0 nt
	s_nop 0
	global_load_dwordx4 v[10:13], v[10:11], off sc0 nt
	v_addc_co_u32_e32 v17, vcc, 0, v163, vcc
	global_load_dwordx4 v[30:33], v[14:15], off sc0 nt
	global_load_dwordx4 v[42:45], v[16:17], off sc0 nt
	ds_read_b128 v[14:17], v142 offset:34816
	s_waitcnt lgkmcnt(0)
	global_store_dwordx4 v[144:145], v[14:17], off offset:768 nt
	ds_read_b128 v[14:17], v146 offset:34816
	s_waitcnt lgkmcnt(0)
	global_store_dwordx4 v[148:149], v[14:17], off offset:768 nt
	ds_read_b128 v[14:17], v150 offset:34816
	s_waitcnt lgkmcnt(0)
	global_store_dwordx4 v[152:153], v[14:17], off offset:768 nt
	ds_read_b128 v[14:17], v158 offset:34816
	s_waitcnt lgkmcnt(0)
	global_store_dwordx4 v[160:161], v[14:17], off offset:768 nt
	s_waitcnt vmcnt(39)
	s_nop 0
	v_mul_f32_e32 v14, 0x43800000, v86
	s_waitcnt vmcnt(38)
	v_mul_f32_e32 v15, 0x43800000, v102
	v_med3_f32 v86, v14, s85, v252
	v_med3_f32 v15, v15, s85, v252
	v_mov_b32_e32 v14, v155
	v_cvt_pk_fp8_f32 v14, v86, v15
	s_waitcnt vmcnt(37)
	v_mul_f32_e32 v16, 0x43800000, v118
	s_waitcnt vmcnt(36)
	v_mul_f32_e32 v17, 0x43800000, v130
	v_med3_f32 v16, v16, s85, v252
	v_med3_f32 v17, v17, s85, v252
	v_cvt_pk_fp8_f32 v14, v16, v17 op_sel:[0,0,1]
	s_waitcnt vmcnt(35)
	v_mul_f32_e32 v15, 0x43800000, v54
	s_waitcnt vmcnt(34)
	v_mul_f32_e32 v16, 0x43800000, v78
	v_med3_f32 v78, v15, s85, v252
	v_med3_f32 v16, v16, s85, v252
	v_mov_b32_e32 v15, v155
	v_cvt_pk_fp8_f32 v15, v78, v16
	s_waitcnt vmcnt(33)
	v_mul_f32_e32 v17, 0x43800000, v98
	s_waitcnt vmcnt(32)
	v_mul_f32_e32 v54, 0x43800000, v114
	v_med3_f32 v17, v17, s85, v252
	v_med3_f32 v54, v54, s85, v252
	v_cvt_pk_fp8_f32 v15, v17, v54 op_sel:[0,0,1]
	s_waitcnt vmcnt(31)
	v_mul_f32_e32 v16, 0x43800000, v22
	s_waitcnt vmcnt(30)
	v_mul_f32_e32 v17, 0x43800000, v46
	v_med3_f32 v54, v16, s85, v252
	v_med3_f32 v17, v17, s85, v252
	v_mov_b32_e32 v16, v155
	v_cvt_pk_fp8_f32 v16, v54, v17
	s_waitcnt vmcnt(27)
	v_mul_f32_e32 v2, 0x43800000, v2
	s_waitcnt vmcnt(26)
	v_mul_f32_e32 v17, 0x43800000, v18
	s_waitcnt vmcnt(25)
	v_mul_f32_e32 v18, 0x43800000, v34
	v_med3_f32 v2, v2, s85, v252
	v_med3_f32 v34, v17, s85, v252
	v_mov_b32_e32 v17, v155
	v_mul_f32_e32 v22, 0x43800000, v66
	v_mul_f32_e32 v46, 0x43800000, v82
	v_cvt_pk_fp8_f32 v17, v2, v34
	v_med3_f32 v22, v22, s85, v252
	v_med3_f32 v46, v46, s85, v252
	v_cvt_pk_fp8_f32 v16, v22, v46 op_sel:[0,0,1]
	s_waitcnt vmcnt(24)
	v_mul_f32_e32 v22, 0x43800000, v50
	v_med3_f32 v18, v18, s85, v252
	v_med3_f32 v22, v22, s85, v252
	v_cvt_pk_fp8_f32 v17, v18, v22 op_sel:[0,0,1]
	v_mul_f32_e32 v2, 0x43800000, v87
	v_med3_f32 v2, v2, s85, v252
	v_mul_f32_e32 v5, 0x43800000, v5
	ds_write_b128 v164, v[14:17]
	v_mul_f32_e32 v14, 0x43800000, v103
	v_med3_f32 v17, v14, s85, v252
	v_mov_b32_e32 v14, v155
	v_cvt_pk_fp8_f32 v14, v2, v17
	v_mul_f32_e32 v15, 0x43800000, v119
	v_mul_f32_e32 v16, 0x43800000, v131
	v_med3_f32 v15, v15, s85, v252
	v_med3_f32 v16, v16, s85, v252
	v_cvt_pk_fp8_f32 v14, v15, v16 op_sel:[0,0,1]
	v_mul_f32_e32 v2, 0x43800000, v55
	v_mul_f32_e32 v15, 0x43800000, v79
	v_med3_f32 v2, v2, s85, v252
	v_med3_f32 v18, v15, s85, v252
	v_mov_b32_e32 v15, v155
	v_cvt_pk_fp8_f32 v15, v2, v18
	v_mul_f32_e32 v16, 0x43800000, v99
	v_mul_f32_e32 v17, 0x43800000, v115
	v_med3_f32 v16, v16, s85, v252
	v_med3_f32 v17, v17, s85, v252
	v_cvt_pk_fp8_f32 v15, v16, v17 op_sel:[0,0,1]
	v_mul_f32_e32 v2, 0x43800000, v23
	v_mul_f32_e32 v16, 0x43800000, v47
	v_med3_f32 v2, v2, s85, v252
	v_med3_f32 v22, v16, s85, v252
	v_mov_b32_e32 v16, v155
	v_cvt_pk_fp8_f32 v16, v2, v22
	v_mul_f32_e32 v17, 0x43800000, v67
	v_mul_f32_e32 v18, 0x43800000, v83
	v_med3_f32 v17, v17, s85, v252
	v_med3_f32 v18, v18, s85, v252
	v_cvt_pk_fp8_f32 v16, v17, v18 op_sel:[0,0,1]
	v_mul_f32_e32 v2, 0x43800000, v3
	v_mul_f32_e32 v3, 0x43800000, v19
	v_mul_f32_e32 v17, 0x43800000, v35
	v_med3_f32 v2, v2, s85, v252
	v_med3_f32 v3, v3, s85, v252
	v_med3_f32 v19, v17, s85, v252
	v_mov_b32_e32 v17, v155
	v_cvt_pk_fp8_f32 v17, v2, v3
	v_mul_f32_e32 v18, 0x43800000, v51
	v_med3_f32 v18, v18, s85, v252
	v_mul_f32_e32 v2, 0x43800000, v88
	v_cvt_pk_fp8_f32 v17, v19, v18 op_sel:[0,0,1]
	v_mul_f32_e32 v3, 0x43800000, v104
	v_med3_f32 v2, v2, s85, v252
	v_med3_f32 v3, v3, s85, v252
	ds_write_b128 v164, v[14:17] offset:272
	v_mul_f32_e32 v14, 0x43800000, v120
	v_med3_f32 v16, v14, s85, v252
	v_mov_b32_e32 v14, v155
	v_cvt_pk_fp8_f32 v14, v2, v3
	v_mul_f32_e32 v15, 0x43800000, v132
	v_med3_f32 v15, v15, s85, v252
	v_mul_f32_e32 v2, 0x43800000, v56
	v_cvt_pk_fp8_f32 v14, v16, v15 op_sel:[0,0,1]
	v_mul_f32_e32 v3, 0x43800000, v80
	v_mul_f32_e32 v15, 0x43800000, v100
	v_med3_f32 v2, v2, s85, v252
	v_med3_f32 v3, v3, s85, v252
	v_med3_f32 v17, v15, s85, v252
	v_mov_b32_e32 v15, v155
	v_cvt_pk_fp8_f32 v15, v2, v3
	v_mul_f32_e32 v16, 0x43800000, v116
	v_med3_f32 v16, v16, s85, v252
	v_mul_f32_e32 v2, 0x43800000, v24
	v_cvt_pk_fp8_f32 v15, v17, v16 op_sel:[0,0,1]
	v_mul_f32_e32 v3, 0x43800000, v48
	v_mul_f32_e32 v16, 0x43800000, v68
	v_med3_f32 v2, v2, s85, v252
	v_med3_f32 v3, v3, s85, v252
	v_med3_f32 v18, v16, s85, v252
	v_mov_b32_e32 v16, v155
	v_cvt_pk_fp8_f32 v16, v2, v3
	v_mul_f32_e32 v17, 0x43800000, v84
	v_med3_f32 v17, v17, s85, v252
	v_mul_f32_e32 v2, 0x43800000, v4
	v_cvt_pk_fp8_f32 v16, v18, v17 op_sel:[0,0,1]
	v_mul_f32_e32 v3, 0x43800000, v20
	v_mul_f32_e32 v17, 0x43800000, v52
	v_med3_f32 v2, v2, s85, v252
	v_med3_f32 v3, v3, s85, v252
	v_med3_f32 v18, v17, s85, v252
	v_mov_b32_e32 v17, v155
	v_cvt_pk_fp8_f32 v17, v2, v3
	v_mul_f32_e32 v4, 0x43800000, v36
	v_med3_f32 v4, v4, s85, v252
	v_mul_f32_e32 v2, 0x43800000, v89
	v_cvt_pk_fp8_f32 v17, v4, v18 op_sel:[0,0,1]
	v_mul_f32_e32 v3, 0x43800000, v105
	v_med3_f32 v3, v3, s85, v252
	v_mul_f32_e32 v4, 0x43800000, v121
	ds_write_b128 v164, v[14:17] offset:544
	v_med3_f32 v15, v2, s85, v252
	v_mov_b32_e32 v2, v155
	v_cvt_pk_fp8_f32 v2, v15, v3
	v_mul_f32_e32 v14, 0x43800000, v133
	v_med3_f32 v4, v4, s85, v252
	v_med3_f32 v14, v14, s85, v252
	v_cvt_pk_fp8_f32 v2, v4, v14 op_sel:[0,0,1]
	v_mul_f32_e32 v3, 0x43800000, v57
	v_mul_f32_e32 v4, 0x43800000, v81
	v_med3_f32 v16, v3, s85, v252
	v_med3_f32 v4, v4, s85, v252
	v_mov_b32_e32 v3, v155
	v_cvt_pk_fp8_f32 v3, v16, v4
	v_mul_f32_e32 v14, 0x43800000, v101
	v_mul_f32_e32 v15, 0x43800000, v117
	v_med3_f32 v14, v14, s85, v252
	v_med3_f32 v15, v15, s85, v252
	v_cvt_pk_fp8_f32 v3, v14, v15 op_sel:[0,0,1]
	v_mul_f32_e32 v4, 0x43800000, v25
	v_mul_f32_e32 v14, 0x43800000, v49
	v_med3_f32 v17, v4, s85, v252
	v_med3_f32 v14, v14, s85, v252
	v_mov_b32_e32 v4, v155
	v_cvt_pk_fp8_f32 v4, v17, v14
	v_mul_f32_e32 v14, 0x43800000, v21
	v_med3_f32 v17, v5, s85, v252
	v_med3_f32 v14, v14, s85, v252
	v_mov_b32_e32 v5, v155
	v_mul_f32_e32 v15, 0x43800000, v69
	v_mul_f32_e32 v16, 0x43800000, v85
	v_cvt_pk_fp8_f32 v5, v17, v14
	v_med3_f32 v15, v15, s85, v252
	v_med3_f32 v16, v16, s85, v252
	v_cvt_pk_fp8_f32 v4, v15, v16 op_sel:[0,0,1]
	v_mul_f32_e32 v15, 0x43800000, v37
	v_mul_f32_e32 v16, 0x43800000, v53
	v_med3_f32 v15, v15, s85, v252
	v_med3_f32 v16, v16, s85, v252
	v_cvt_pk_fp8_f32 v5, v15, v16 op_sel:[0,0,1]
	ds_write_b128 v164, v[2:5] offset:816
	s_waitcnt lgkmcnt(0)
	s_barrier
	s_mov_b32 s0, 0x1800000
	v_add_co_u32_e32 v2, vcc, s0, v162
	s_mov_b32 s0, 0x1804000
	s_nop 0
	v_addc_co_u32_e32 v3, vcc, 0, v163, vcc
	v_add_co_u32_e32 v4, vcc, s0, v162
	s_mov_b32 s0, 0x1808000
	s_nop 0
	v_addc_co_u32_e32 v5, vcc, 0, v163, vcc
	global_load_dwordx4 v[82:85], v[2:3], off sc0 nt
	global_load_dwordx4 v[98:101], v[4:5], off sc0 nt
	v_add_co_u32_e32 v2, vcc, s0, v162
	s_mov_b32 s0, 0x180c000
	s_nop 0
	v_addc_co_u32_e32 v3, vcc, 0, v163, vcc
	v_add_co_u32_e32 v4, vcc, s0, v162
	s_mov_b32 s0, 0x1810000
	s_nop 0
	v_addc_co_u32_e32 v5, vcc, 0, v163, vcc
	global_load_dwordx4 v[114:117], v[2:3], off sc0 nt
	global_load_dwordx4 v[118:121], v[4:5], off sc0 nt
	v_add_co_u32_e32 v2, vcc, s0, v162
	s_mov_b32 s0, 0x1814000
	s_nop 0
	v_addc_co_u32_e32 v3, vcc, 0, v163, vcc
	v_add_co_u32_e32 v4, vcc, s0, v162
	s_mov_b32 s0, 0x1818000
	s_nop 0
	v_addc_co_u32_e32 v5, vcc, 0, v163, vcc
	global_load_dwordx4 v[50:53], v[2:3], off sc0 nt
	global_load_dwordx4 v[66:69], v[4:5], off sc0 nt
	v_add_co_u32_e32 v2, vcc, s0, v162
	s_mov_b32 s0, 0x181c000
	s_nop 0
	v_addc_co_u32_e32 v3, vcc, 0, v163, vcc
	v_add_co_u32_e32 v4, vcc, s0, v162
	s_mov_b32 s0, 0x1820000
	s_nop 0
	v_addc_co_u32_e32 v5, vcc, 0, v163, vcc
	global_load_dwordx4 v[86:89], v[2:3], off sc0 nt
	global_load_dwordx4 v[102:105], v[4:5], off sc0 nt
	v_add_co_u32_e32 v2, vcc, s0, v162
	s_mov_b32 s0, 0x1824000
	s_nop 0
	v_addc_co_u32_e32 v3, vcc, 0, v163, vcc
	v_add_co_u32_e32 v4, vcc, s0, v162
	s_mov_b32 s0, 0x1828000
	s_nop 0
	v_addc_co_u32_e32 v5, vcc, 0, v163, vcc
	global_load_dwordx4 v[18:21], v[2:3], off sc0 nt
	global_load_dwordx4 v[34:37], v[4:5], off sc0 nt
	v_add_co_u32_e32 v2, vcc, s0, v162
	s_mov_b32 s0, 0x182c000
	s_nop 0
	v_addc_co_u32_e32 v3, vcc, 0, v163, vcc
	v_add_co_u32_e32 v4, vcc, s0, v162
	s_mov_b32 s0, 0x1830000
	s_nop 0
	v_addc_co_u32_e32 v5, vcc, 0, v163, vcc
	global_load_dwordx4 v[54:57], v[2:3], off sc0 nt
	global_load_dwordx4 v[78:81], v[4:5], off sc0 nt
	v_add_co_u32_e32 v2, vcc, s0, v162
	s_mov_b32 s0, 0x1834000
	s_nop 0
	v_addc_co_u32_e32 v3, vcc, 0, v163, vcc
	v_add_co_u32_e32 v14, vcc, s0, v162
	s_mov_b32 s0, 0x1838000
	s_nop 0
	v_addc_co_u32_e32 v15, vcc, 0, v163, vcc
	v_add_co_u32_e32 v22, vcc, s0, v162
	s_mov_b32 s0, 0x183c000
	s_nop 0
	v_addc_co_u32_e32 v23, vcc, 0, v163, vcc
	v_add_co_u32_e32 v46, vcc, s0, v162
	global_load_dwordx4 v[2:5], v[2:3], off sc0 nt
	s_nop 0
	global_load_dwordx4 v[14:17], v[14:15], off sc0 nt
	v_addc_co_u32_e32 v47, vcc, 0, v163, vcc
	global_load_dwordx4 v[22:25], v[22:23], off sc0 nt
	s_nop 0
	global_load_dwordx4 v[46:49], v[46:47], off sc0 nt
	ds_read_b128 v[130:133], v142
	s_waitcnt lgkmcnt(0)
	global_store_dwordx4 v[144:145], v[130:133], off offset:1024 nt
	ds_read_b128 v[130:133], v146
	s_waitcnt lgkmcnt(0)
	global_store_dwordx4 v[148:149], v[130:133], off offset:1024 nt
	ds_read_b128 v[130:133], v150
	s_waitcnt lgkmcnt(0)
	global_store_dwordx4 v[152:153], v[130:133], off offset:1024 nt
	ds_read_b128 v[130:133], v158
	s_waitcnt lgkmcnt(0)
	global_store_dwordx4 v[160:161], v[130:133], off offset:1024 nt
	s_waitcnt vmcnt(39)
	v_mul_f32_e32 v90, 0x43800000, v90
	s_waitcnt vmcnt(38)
	v_mul_f32_e32 v106, 0x43800000, v106
	s_waitcnt vmcnt(35)
	v_mul_f32_e32 v58, 0x43800000, v58
	s_waitcnt vmcnt(34)
	v_mul_f32_e32 v70, 0x43800000, v70
	s_waitcnt vmcnt(31)
	v_mul_f32_e32 v26, 0x43800000, v26
	s_waitcnt vmcnt(30)
	v_mul_f32_e32 v38, 0x43800000, v38
	s_waitcnt vmcnt(27)
	v_mul_f32_e32 v6, 0x43800000, v6
	s_waitcnt vmcnt(26)
	v_mul_f32_e32 v10, 0x43800000, v10
	v_med3_f32 v90, v90, s85, v252
	v_med3_f32 v106, v106, s85, v252
	v_mov_b32_e32 v130, v155
	v_med3_f32 v58, v58, s85, v252
	v_med3_f32 v70, v70, s85, v252
	v_mov_b32_e32 v131, v155
	v_med3_f32 v26, v26, s85, v252
	v_med3_f32 v38, v38, s85, v252
	v_mov_b32_e32 v132, v155
	v_med3_f32 v6, v6, s85, v252
	v_med3_f32 v10, v10, s85, v252
	v_mov_b32_e32 v133, v155
	v_cvt_pk_fp8_f32 v130, v90, v106
	v_cvt_pk_fp8_f32 v131, v58, v70
	v_cvt_pk_fp8_f32 v132, v26, v38
	v_cvt_pk_fp8_f32 v133, v6, v10
	v_mul_f32_e32 v122, 0x43800000, v122
	v_mul_f32_e32 v126, 0x43800000, v126
	v_mul_f32_e32 v90, 0x43800000, v94
	v_mul_f32_e32 v94, 0x43800000, v110
	v_mul_f32_e32 v58, 0x43800000, v62
	v_mul_f32_e32 v62, 0x43800000, v74
	s_waitcnt vmcnt(25)
	v_mul_f32_e32 v26, 0x43800000, v30
	s_waitcnt vmcnt(24)
	v_mul_f32_e32 v30, 0x43800000, v42
	v_med3_f32 v122, v122, s85, v252
	v_med3_f32 v126, v126, s85, v252
	v_med3_f32 v90, v90, s85, v252
	v_med3_f32 v94, v94, s85, v252
	v_med3_f32 v58, v58, s85, v252
	v_med3_f32 v62, v62, s85, v252
	v_med3_f32 v26, v26, s85, v252
	v_med3_f32 v30, v30, s85, v252
	v_cvt_pk_fp8_f32 v130, v122, v126 op_sel:[0,0,1]
	v_cvt_pk_fp8_f32 v131, v90, v94 op_sel:[0,0,1]
	v_cvt_pk_fp8_f32 v132, v58, v62 op_sel:[0,0,1]
	v_cvt_pk_fp8_f32 v133, v26, v30 op_sel:[0,0,1]
	v_mul_f32_e32 v6, 0x43800000, v91
	v_mul_f32_e32 v10, 0x43800000, v107
	v_med3_f32 v6, v6, s85, v252
	ds_write_b128 v164, v[130:133] offset:34816
	v_med3_f32 v10, v10, s85, v252
	v_mov_b32_e32 v130, v155
	v_cvt_pk_fp8_f32 v130, v6, v10
	v_mul_f32_e32 v6, 0x43800000, v59
	v_mul_f32_e32 v10, 0x43800000, v71
	v_med3_f32 v6, v6, s85, v252
	v_med3_f32 v10, v10, s85, v252
	v_mov_b32_e32 v131, v155
	v_cvt_pk_fp8_f32 v131, v6, v10
	v_mul_f32_e32 v6, 0x43800000, v27
	v_mul_f32_e32 v10, 0x43800000, v39
	v_med3_f32 v6, v6, s85, v252
	v_med3_f32 v10, v10, s85, v252
	v_mov_b32_e32 v132, v155
	v_mul_f32_e32 v26, 0x43800000, v123
	v_mul_f32_e32 v30, 0x43800000, v127
	v_cvt_pk_fp8_f32 v132, v6, v10
	v_mul_f32_e32 v6, 0x43800000, v7
	v_mul_f32_e32 v7, 0x43800000, v11
	v_med3_f32 v26, v26, s85, v252
	v_med3_f32 v30, v30, s85, v252
	v_med3_f32 v6, v6, s85, v252
	v_med3_f32 v7, v7, s85, v252
	v_mov_b32_e32 v133, v155
	v_cvt_pk_fp8_f32 v130, v26, v30 op_sel:[0,0,1]
	v_mul_f32_e32 v26, 0x43800000, v95
	v_mul_f32_e32 v30, 0x43800000, v111
	v_cvt_pk_fp8_f32 v133, v6, v7
	v_med3_f32 v26, v26, s85, v252
	v_med3_f32 v30, v30, s85, v252
	v_cvt_pk_fp8_f32 v131, v26, v30 op_sel:[0,0,1]
	v_mul_f32_e32 v26, 0x43800000, v63
	v_mul_f32_e32 v27, 0x43800000, v75
	v_mul_f32_e32 v10, 0x43800000, v31
	v_mul_f32_e32 v11, 0x43800000, v43
	v_med3_f32 v26, v26, s85, v252
	v_med3_f32 v27, v27, s85, v252
	v_med3_f32 v10, v10, s85, v252
	v_med3_f32 v11, v11, s85, v252
	v_cvt_pk_fp8_f32 v132, v26, v27 op_sel:[0,0,1]
	v_cvt_pk_fp8_f32 v133, v10, v11 op_sel:[0,0,1]
	v_mul_f32_e32 v6, 0x43800000, v92
	v_mul_f32_e32 v7, 0x43800000, v108
	v_med3_f32 v6, v6, s85, v252
	ds_write_b128 v164, v[130:133] offset:35088
	v_med3_f32 v7, v7, s85, v252
	v_mov_b32_e32 v130, v155
	v_cvt_pk_fp8_f32 v130, v6, v7
	v_mul_f32_e32 v6, 0x43800000, v60
	v_mul_f32_e32 v7, 0x43800000, v72
	v_med3_f32 v6, v6, s85, v252
	v_med3_f32 v7, v7, s85, v252
	v_mov_b32_e32 v131, v155
	v_mul_f32_e32 v10, 0x43800000, v124
	v_mul_f32_e32 v11, 0x43800000, v128
	v_cvt_pk_fp8_f32 v131, v6, v7
	v_mul_f32_e32 v6, 0x43800000, v28
	v_mul_f32_e32 v7, 0x43800000, v40
	v_med3_f32 v10, v10, s85, v252
	v_med3_f32 v11, v11, s85, v252
	v_med3_f32 v6, v6, s85, v252
	v_med3_f32 v7, v7, s85, v252
	v_mov_b32_e32 v132, v155
	v_cvt_pk_fp8_f32 v130, v10, v11 op_sel:[0,0,1]
	v_mul_f32_e32 v10, 0x43800000, v96
	v_mul_f32_e32 v11, 0x43800000, v112
	v_cvt_pk_fp8_f32 v132, v6, v7
	v_med3_f32 v10, v10, s85, v252
	v_med3_f32 v11, v11, s85, v252
	v_mul_f32_e32 v6, 0x43800000, v8
	v_mul_f32_e32 v7, 0x43800000, v12
	v_cvt_pk_fp8_f32 v131, v10, v11 op_sel:[0,0,1]
	v_mul_f32_e32 v10, 0x43800000, v64
	v_mul_f32_e32 v11, 0x43800000, v76
	v_med3_f32 v6, v6, s85, v252
	v_med3_f32 v7, v7, s85, v252
	v_mov_b32_e32 v133, v155
	v_med3_f32 v10, v10, s85, v252
	v_med3_f32 v11, v11, s85, v252
	v_cvt_pk_fp8_f32 v133, v6, v7
	v_mul_f32_e32 v6, 0x43800000, v93
	v_mul_f32_e32 v7, 0x43800000, v109
	v_cvt_pk_fp8_f32 v132, v10, v11 op_sel:[0,0,1]
	v_med3_f32 v11, v6, s85, v252
	v_med3_f32 v7, v7, s85, v252
	v_mov_b32_e32 v6, v155
	v_mul_f32_e32 v8, 0x43800000, v32
	v_mul_f32_e32 v10, 0x43800000, v44
	v_cvt_pk_fp8_f32 v6, v11, v7
	v_med3_f32 v8, v8, s85, v252
	v_med3_f32 v10, v10, s85, v252
	v_cvt_pk_fp8_f32 v133, v8, v10 op_sel:[0,0,1]
	v_mul_f32_e32 v8, 0x43800000, v125
	v_mul_f32_e32 v10, 0x43800000, v129
	v_med3_f32 v8, v8, s85, v252
	v_med3_f32 v10, v10, s85, v252
	v_cvt_pk_fp8_f32 v6, v8, v10 op_sel:[0,0,1]
	v_mul_f32_e32 v7, 0x43800000, v61
	v_mul_f32_e32 v8, 0x43800000, v73
	v_med3_f32 v12, v7, s85, v252
	v_med3_f32 v8, v8, s85, v252
	v_mov_b32_e32 v7, v155
	v_cvt_pk_fp8_f32 v7, v12, v8
	v_mul_f32_e32 v10, 0x43800000, v97
	v_mul_f32_e32 v11, 0x43800000, v113
	v_med3_f32 v10, v10, s85, v252
	v_med3_f32 v11, v11, s85, v252
	v_cvt_pk_fp8_f32 v7, v10, v11 op_sel:[0,0,1]
	v_mul_f32_e32 v8, 0x43800000, v29
	v_mul_f32_e32 v10, 0x43800000, v41
	v_med3_f32 v26, v8, s85, v252
	v_med3_f32 v10, v10, s85, v252
	v_mov_b32_e32 v8, v155
	v_cvt_pk_fp8_f32 v8, v26, v10
	v_mul_f32_e32 v9, 0x43800000, v9
	v_mul_f32_e32 v10, 0x43800000, v13
	v_med3_f32 v13, v9, s85, v252
	v_med3_f32 v10, v10, s85, v252
	v_mov_b32_e32 v9, v155
	v_mul_f32_e32 v11, 0x43800000, v65
	v_mul_f32_e32 v12, 0x43800000, v77
	v_cvt_pk_fp8_f32 v9, v13, v10
	v_med3_f32 v11, v11, s85, v252
	v_med3_f32 v12, v12, s85, v252
	v_cvt_pk_fp8_f32 v8, v11, v12 op_sel:[0,0,1]
	v_mul_f32_e32 v11, 0x43800000, v33
	v_mul_f32_e32 v12, 0x43800000, v45
	v_med3_f32 v11, v11, s85, v252
	v_med3_f32 v12, v12, s85, v252
	v_cvt_pk_fp8_f32 v9, v11, v12 op_sel:[0,0,1]
	ds_write_b128 v164, v[130:133] offset:35360
	ds_write_b128 v164, v[6:9] offset:35632
	s_waitcnt lgkmcnt(0)
	s_barrier
	s_mov_b32 s0, 0x1c00000
	v_add_co_u32_e32 v6, vcc, s0, v162
	s_mov_b32 s0, 0x1c04000
	s_nop 0
	v_addc_co_u32_e32 v7, vcc, 0, v163, vcc
	v_add_co_u32_e32 v8, vcc, s0, v162
	s_mov_b32 s0, 0x1c08000
	s_nop 0
	v_addc_co_u32_e32 v9, vcc, 0, v163, vcc
	global_load_dwordx4 v[90:93], v[6:7], off sc0 nt
	global_load_dwordx4 v[106:109], v[8:9], off sc0 nt
	v_add_co_u32_e32 v6, vcc, s0, v162
	s_mov_b32 s0, 0x1c0c000
	s_nop 0
	v_addc_co_u32_e32 v7, vcc, 0, v163, vcc
	v_add_co_u32_e32 v8, vcc, s0, v162
	s_mov_b32 s0, 0x1c10000
	s_nop 0
	v_addc_co_u32_e32 v9, vcc, 0, v163, vcc
	global_load_dwordx4 v[122:125], v[6:7], off sc0 nt
	global_load_dwordx4 v[126:129], v[8:9], off sc0 nt
	v_add_co_u32_e32 v6, vcc, s0, v162
	s_mov_b32 s0, 0x1c14000
	s_nop 0
	v_addc_co_u32_e32 v7, vcc, 0, v163, vcc
	v_add_co_u32_e32 v8, vcc, s0, v162
	s_mov_b32 s0, 0x1c18000
	s_nop 0
	v_addc_co_u32_e32 v9, vcc, 0, v163, vcc
	global_load_dwordx4 v[58:61], v[6:7], off sc0 nt
	global_load_dwordx4 v[70:73], v[8:9], off sc0 nt
	v_add_co_u32_e32 v6, vcc, s0, v162
	s_mov_b32 s0, 0x1c1c000
	s_nop 0
	v_addc_co_u32_e32 v7, vcc, 0, v163, vcc
	v_add_co_u32_e32 v8, vcc, s0, v162
	s_mov_b32 s0, 0x1c20000
	s_nop 0
	v_addc_co_u32_e32 v9, vcc, 0, v163, vcc
	global_load_dwordx4 v[94:97], v[6:7], off sc0 nt
	global_load_dwordx4 v[110:113], v[8:9], off sc0 nt
	v_add_co_u32_e32 v6, vcc, s0, v162
	s_mov_b32 s0, 0x1c24000
	s_nop 0
	v_addc_co_u32_e32 v7, vcc, 0, v163, vcc
	v_add_co_u32_e32 v8, vcc, s0, v162
	s_mov_b32 s0, 0x1c28000
	s_nop 0
	v_addc_co_u32_e32 v9, vcc, 0, v163, vcc
	global_load_dwordx4 v[26:29], v[6:7], off sc0 nt
	global_load_dwordx4 v[38:41], v[8:9], off sc0 nt
	v_add_co_u32_e32 v6, vcc, s0, v162
	s_mov_b32 s0, 0x1c2c000
	s_nop 0
	v_addc_co_u32_e32 v7, vcc, 0, v163, vcc
	v_add_co_u32_e32 v8, vcc, s0, v162
	s_mov_b32 s0, 0x1c30000
	s_nop 0
	v_addc_co_u32_e32 v9, vcc, 0, v163, vcc
	global_load_dwordx4 v[62:65], v[6:7], off sc0 nt
	global_load_dwordx4 v[74:77], v[8:9], off sc0 nt
	v_add_co_u32_e32 v6, vcc, s0, v162
	s_mov_b32 s0, 0x1c34000
	s_nop 0
	v_addc_co_u32_e32 v7, vcc, 0, v163, vcc
	v_add_co_u32_e32 v10, vcc, s0, v162
	s_mov_b32 s0, 0x1c38000
	s_nop 0
	v_addc_co_u32_e32 v11, vcc, 0, v163, vcc
	v_add_co_u32_e32 v30, vcc, s0, v162
	s_mov_b32 s0, 0x1c3c000
	s_nop 0
	v_addc_co_u32_e32 v31, vcc, 0, v163, vcc
	v_add_co_u32_e32 v42, vcc, s0, v162
	global_load_dwordx4 v[6:9], v[6:7], off sc0 nt
	s_nop 0
	global_load_dwordx4 v[10:13], v[10:11], off sc0 nt
	v_addc_co_u32_e32 v43, vcc, 0, v163, vcc
	global_load_dwordx4 v[30:33], v[30:31], off sc0 nt
	s_nop 0
	global_load_dwordx4 v[42:45], v[42:43], off sc0 nt
	ds_read_b128 v[130:133], v142 offset:34816
	s_waitcnt lgkmcnt(0)
	global_store_dwordx4 v[144:145], v[130:133], off offset:1280 nt
	ds_read_b128 v[130:133], v146 offset:34816
	s_waitcnt lgkmcnt(0)
	global_store_dwordx4 v[148:149], v[130:133], off offset:1280 nt
	ds_read_b128 v[130:133], v150 offset:34816
	s_waitcnt lgkmcnt(0)
	global_store_dwordx4 v[152:153], v[130:133], off offset:1280 nt
	ds_read_b128 v[130:133], v158 offset:34816
	s_waitcnt lgkmcnt(0)
	global_store_dwordx4 v[160:161], v[130:133], off offset:1280 nt
	s_waitcnt vmcnt(39)
	v_mul_f32_e32 v82, 0x43800000, v82
	s_waitcnt vmcnt(38)
	v_mul_f32_e32 v98, 0x43800000, v98
	s_waitcnt vmcnt(35)
	v_mul_f32_e32 v50, 0x43800000, v50
	s_waitcnt vmcnt(34)
	v_mul_f32_e32 v66, 0x43800000, v66
	s_waitcnt vmcnt(31)
	v_mul_f32_e32 v18, 0x43800000, v18
	s_waitcnt vmcnt(30)
	v_mul_f32_e32 v34, 0x43800000, v34
	s_waitcnt vmcnt(27)
	v_mul_f32_e32 v2, 0x43800000, v2
	s_waitcnt vmcnt(26)
	v_mul_f32_e32 v14, 0x43800000, v14
	v_med3_f32 v82, v82, s85, v252
	v_med3_f32 v98, v98, s85, v252
	v_mov_b32_e32 v130, v155
	v_med3_f32 v50, v50, s85, v252
	v_med3_f32 v66, v66, s85, v252
	v_mov_b32_e32 v131, v155
	v_med3_f32 v18, v18, s85, v252
	v_med3_f32 v34, v34, s85, v252
	v_mov_b32_e32 v132, v155
	v_med3_f32 v2, v2, s85, v252
	v_med3_f32 v14, v14, s85, v252
	v_mov_b32_e32 v133, v155
	v_cvt_pk_fp8_f32 v130, v82, v98
	v_cvt_pk_fp8_f32 v131, v50, v66
	v_cvt_pk_fp8_f32 v132, v18, v34
	v_cvt_pk_fp8_f32 v133, v2, v14
	v_mul_f32_e32 v114, 0x43800000, v114
	v_mul_f32_e32 v118, 0x43800000, v118
	v_mul_f32_e32 v82, 0x43800000, v86
	v_mul_f32_e32 v86, 0x43800000, v102
	v_mul_f32_e32 v50, 0x43800000, v54
	v_mul_f32_e32 v54, 0x43800000, v78
	s_waitcnt vmcnt(25)
	v_mul_f32_e32 v18, 0x43800000, v22
	s_waitcnt vmcnt(24)
	v_mul_f32_e32 v22, 0x43800000, v46
	v_med3_f32 v114, v114, s85, v252
	v_med3_f32 v118, v118, s85, v252
	v_med3_f32 v82, v82, s85, v252
	v_med3_f32 v86, v86, s85, v252
	v_med3_f32 v50, v50, s85, v252
	v_med3_f32 v54, v54, s85, v252
	v_med3_f32 v18, v18, s85, v252
	v_med3_f32 v22, v22, s85, v252
	v_cvt_pk_fp8_f32 v130, v114, v118 op_sel:[0,0,1]
	v_cvt_pk_fp8_f32 v131, v82, v86 op_sel:[0,0,1]
	v_cvt_pk_fp8_f32 v132, v50, v54 op_sel:[0,0,1]
	v_cvt_pk_fp8_f32 v133, v18, v22 op_sel:[0,0,1]
	v_mul_f32_e32 v2, 0x43800000, v83
	v_mul_f32_e32 v14, 0x43800000, v99
	v_med3_f32 v2, v2, s85, v252
	ds_write_b128 v164, v[130:133]
	v_med3_f32 v14, v14, s85, v252
	v_mov_b32_e32 v130, v155
	v_cvt_pk_fp8_f32 v130, v2, v14
	v_mul_f32_e32 v2, 0x43800000, v51
	v_mul_f32_e32 v14, 0x43800000, v67
	v_med3_f32 v2, v2, s85, v252
	v_med3_f32 v14, v14, s85, v252
	v_mov_b32_e32 v131, v155
	v_cvt_pk_fp8_f32 v131, v2, v14
	v_mul_f32_e32 v2, 0x43800000, v19
	v_mul_f32_e32 v14, 0x43800000, v35
	v_med3_f32 v2, v2, s85, v252
	v_med3_f32 v14, v14, s85, v252
	v_mov_b32_e32 v132, v155
	v_mul_f32_e32 v18, 0x43800000, v115
	v_mul_f32_e32 v22, 0x43800000, v119
	v_cvt_pk_fp8_f32 v132, v2, v14
	v_mul_f32_e32 v2, 0x43800000, v3
	v_mul_f32_e32 v3, 0x43800000, v15
	v_med3_f32 v18, v18, s85, v252
	v_med3_f32 v22, v22, s85, v252
	v_med3_f32 v2, v2, s85, v252
	v_med3_f32 v3, v3, s85, v252
	v_mov_b32_e32 v133, v155
	v_cvt_pk_fp8_f32 v130, v18, v22 op_sel:[0,0,1]
	v_mul_f32_e32 v18, 0x43800000, v87
	v_mul_f32_e32 v22, 0x43800000, v103
	v_cvt_pk_fp8_f32 v133, v2, v3
	v_med3_f32 v18, v18, s85, v252
	v_med3_f32 v22, v22, s85, v252
	v_cvt_pk_fp8_f32 v131, v18, v22 op_sel:[0,0,1]
	v_mul_f32_e32 v18, 0x43800000, v55
	v_mul_f32_e32 v19, 0x43800000, v79
	v_mul_f32_e32 v14, 0x43800000, v23
	v_mul_f32_e32 v15, 0x43800000, v47
	v_med3_f32 v18, v18, s85, v252
	v_med3_f32 v19, v19, s85, v252
	v_med3_f32 v14, v14, s85, v252
	v_med3_f32 v15, v15, s85, v252
	v_cvt_pk_fp8_f32 v132, v18, v19 op_sel:[0,0,1]
	v_cvt_pk_fp8_f32 v133, v14, v15 op_sel:[0,0,1]
	v_mul_f32_e32 v2, 0x43800000, v84
	v_mul_f32_e32 v3, 0x43800000, v100
	v_med3_f32 v2, v2, s85, v252
	ds_write_b128 v164, v[130:133] offset:272
	v_med3_f32 v3, v3, s85, v252
	v_mov_b32_e32 v130, v155
	v_cvt_pk_fp8_f32 v130, v2, v3
	v_mul_f32_e32 v2, 0x43800000, v52
	v_mul_f32_e32 v3, 0x43800000, v68
	v_med3_f32 v2, v2, s85, v252
	v_med3_f32 v3, v3, s85, v252
	v_mov_b32_e32 v131, v155
	v_mul_f32_e32 v14, 0x43800000, v116
	v_mul_f32_e32 v15, 0x43800000, v120
	v_cvt_pk_fp8_f32 v131, v2, v3
	v_mul_f32_e32 v2, 0x43800000, v20
	v_mul_f32_e32 v3, 0x43800000, v36
	v_med3_f32 v14, v14, s85, v252
	v_med3_f32 v15, v15, s85, v252
	v_med3_f32 v2, v2, s85, v252
	v_med3_f32 v3, v3, s85, v252
	v_mov_b32_e32 v132, v155
	v_cvt_pk_fp8_f32 v130, v14, v15 op_sel:[0,0,1]
	v_mul_f32_e32 v14, 0x43800000, v88
	v_mul_f32_e32 v15, 0x43800000, v104
	v_cvt_pk_fp8_f32 v132, v2, v3
	v_med3_f32 v14, v14, s85, v252
	v_med3_f32 v15, v15, s85, v252
	v_mul_f32_e32 v2, 0x43800000, v4
	v_mul_f32_e32 v3, 0x43800000, v16
	v_cvt_pk_fp8_f32 v131, v14, v15 op_sel:[0,0,1]
	v_mul_f32_e32 v14, 0x43800000, v56
	v_mul_f32_e32 v15, 0x43800000, v80
	v_med3_f32 v2, v2, s85, v252
	v_med3_f32 v3, v3, s85, v252
	v_mov_b32_e32 v133, v155
	v_med3_f32 v14, v14, s85, v252
	v_med3_f32 v15, v15, s85, v252
	v_cvt_pk_fp8_f32 v133, v2, v3
	v_mul_f32_e32 v2, 0x43800000, v85
	v_mul_f32_e32 v3, 0x43800000, v101
	v_cvt_pk_fp8_f32 v132, v14, v15 op_sel:[0,0,1]
	v_med3_f32 v15, v2, s85, v252
	v_med3_f32 v3, v3, s85, v252
	v_mov_b32_e32 v2, v155
	v_mul_f32_e32 v4, 0x43800000, v24
	v_mul_f32_e32 v14, 0x43800000, v48
	v_cvt_pk_fp8_f32 v2, v15, v3
	v_med3_f32 v4, v4, s85, v252
	v_med3_f32 v14, v14, s85, v252
	v_cvt_pk_fp8_f32 v133, v4, v14 op_sel:[0,0,1]
	v_mul_f32_e32 v4, 0x43800000, v117
	v_mul_f32_e32 v14, 0x43800000, v121
	v_med3_f32 v4, v4, s85, v252
	v_med3_f32 v14, v14, s85, v252
	v_cvt_pk_fp8_f32 v2, v4, v14 op_sel:[0,0,1]
	v_mul_f32_e32 v3, 0x43800000, v53
	v_mul_f32_e32 v4, 0x43800000, v69
	v_med3_f32 v16, v3, s85, v252
	v_med3_f32 v4, v4, s85, v252
	v_mov_b32_e32 v3, v155
	v_cvt_pk_fp8_f32 v3, v16, v4
	v_mul_f32_e32 v14, 0x43800000, v89
	v_mul_f32_e32 v15, 0x43800000, v105
	v_med3_f32 v14, v14, s85, v252
	v_med3_f32 v15, v15, s85, v252
	v_cvt_pk_fp8_f32 v3, v14, v15 op_sel:[0,0,1]
	v_mul_f32_e32 v4, 0x43800000, v21
	v_mul_f32_e32 v14, 0x43800000, v37
	v_med3_f32 v18, v4, s85, v252
	v_med3_f32 v14, v14, s85, v252
	v_mov_b32_e32 v4, v155
	v_cvt_pk_fp8_f32 v4, v18, v14
	v_mul_f32_e32 v5, 0x43800000, v5
	v_mul_f32_e32 v14, 0x43800000, v17
	v_med3_f32 v17, v5, s85, v252
	v_med3_f32 v14, v14, s85, v252
	v_mov_b32_e32 v5, v155
	v_mul_f32_e32 v15, 0x43800000, v57
	v_mul_f32_e32 v16, 0x43800000, v81
	v_cvt_pk_fp8_f32 v5, v17, v14
	v_med3_f32 v15, v15, s85, v252
	v_med3_f32 v16, v16, s85, v252
	v_cvt_pk_fp8_f32 v4, v15, v16 op_sel:[0,0,1]
	v_mul_f32_e32 v15, 0x43800000, v25
	v_mul_f32_e32 v16, 0x43800000, v49
	v_med3_f32 v15, v15, s85, v252
	v_med3_f32 v16, v16, s85, v252
	v_cvt_pk_fp8_f32 v5, v15, v16 op_sel:[0,0,1]
	ds_write_b128 v164, v[130:133] offset:544
	ds_write_b128 v164, v[2:5] offset:816
	s_waitcnt lgkmcnt(0)
	s_barrier
	ds_read_b128 v[2:5], v142
	s_waitcnt lgkmcnt(0)
	global_store_dwordx4 v[144:145], v[2:5], off offset:1536 nt
	ds_read_b128 v[2:5], v146
	s_waitcnt lgkmcnt(0)
	global_store_dwordx4 v[148:149], v[2:5], off offset:1536 nt
	ds_read_b128 v[2:5], v150
	s_waitcnt lgkmcnt(0)
	global_store_dwordx4 v[152:153], v[2:5], off offset:1536 nt
	ds_read_b128 v[2:5], v158
	s_waitcnt lgkmcnt(0)
	global_store_dwordx4 v[160:161], v[2:5], off offset:1536 nt
	s_waitcnt vmcnt(23)
	s_nop 0
	v_mul_f32_e32 v2, 0x43800000, v90
	s_waitcnt vmcnt(22)
	v_mul_f32_e32 v3, 0x43800000, v106
	v_med3_f32 v14, v2, s85, v252
	v_med3_f32 v3, v3, s85, v252
	v_mov_b32_e32 v2, v155
	v_cvt_pk_fp8_f32 v2, v14, v3
	s_waitcnt vmcnt(21)
	v_mul_f32_e32 v4, 0x43800000, v122
	s_waitcnt vmcnt(20)
	v_mul_f32_e32 v5, 0x43800000, v126
	v_med3_f32 v4, v4, s85, v252
	v_med3_f32 v5, v5, s85, v252
	v_cvt_pk_fp8_f32 v2, v4, v5 op_sel:[0,0,1]
	s_waitcnt vmcnt(19)
	v_mul_f32_e32 v3, 0x43800000, v58
	s_waitcnt vmcnt(18)
	v_mul_f32_e32 v4, 0x43800000, v70
	v_med3_f32 v15, v3, s85, v252
	v_med3_f32 v4, v4, s85, v252
	v_mov_b32_e32 v3, v155
	v_cvt_pk_fp8_f32 v3, v15, v4
	s_waitcnt vmcnt(17)
	v_mul_f32_e32 v5, 0x43800000, v94
	s_waitcnt vmcnt(16)
	v_mul_f32_e32 v14, 0x43800000, v110
	v_med3_f32 v5, v5, s85, v252
	v_med3_f32 v14, v14, s85, v252
	v_cvt_pk_fp8_f32 v3, v5, v14 op_sel:[0,0,1]
	s_waitcnt vmcnt(15)
	v_mul_f32_e32 v4, 0x43800000, v26
	s_waitcnt vmcnt(14)
	v_mul_f32_e32 v5, 0x43800000, v38
	v_med3_f32 v16, v4, s85, v252
	v_med3_f32 v5, v5, s85, v252
	v_mov_b32_e32 v4, v155
	v_cvt_pk_fp8_f32 v4, v16, v5
	s_waitcnt vmcnt(13)
	v_mul_f32_e32 v14, 0x43800000, v62
	s_waitcnt vmcnt(12)
	v_mul_f32_e32 v15, 0x43800000, v74
	v_med3_f32 v14, v14, s85, v252
	v_med3_f32 v15, v15, s85, v252
	s_waitcnt vmcnt(11)
	v_mul_f32_e32 v5, 0x43800000, v6
	s_waitcnt vmcnt(10)
	v_mul_f32_e32 v6, 0x43800000, v10
	v_cvt_pk_fp8_f32 v4, v14, v15 op_sel:[0,0,1]
	v_med3_f32 v15, v5, s85, v252
	v_med3_f32 v6, v6, s85, v252
	v_mov_b32_e32 v5, v155
	v_cvt_pk_fp8_f32 v5, v15, v6
	s_waitcnt vmcnt(9)
	v_mul_f32_e32 v10, 0x43800000, v30
	s_waitcnt vmcnt(8)
	v_mul_f32_e32 v14, 0x43800000, v42
	v_med3_f32 v10, v10, s85, v252
	v_med3_f32 v14, v14, s85, v252
	v_cvt_pk_fp8_f32 v5, v10, v14 op_sel:[0,0,1]
	ds_write_b128 v164, v[2:5] offset:34816
	v_mul_f32_e32 v2, 0x43800000, v91
	v_mul_f32_e32 v3, 0x43800000, v107
	v_med3_f32 v6, v2, s85, v252
	v_med3_f32 v3, v3, s85, v252
	v_mov_b32_e32 v2, v155
	v_cvt_pk_fp8_f32 v2, v6, v3
	v_mul_f32_e32 v4, 0x43800000, v123
	v_mul_f32_e32 v5, 0x43800000, v127
	v_med3_f32 v4, v4, s85, v252
	v_med3_f32 v5, v5, s85, v252
	v_cvt_pk_fp8_f32 v2, v4, v5 op_sel:[0,0,1]
	v_mul_f32_e32 v3, 0x43800000, v59
	v_mul_f32_e32 v4, 0x43800000, v71
	v_med3_f32 v10, v3, s85, v252
	v_med3_f32 v4, v4, s85, v252
	v_mov_b32_e32 v3, v155
	v_cvt_pk_fp8_f32 v3, v10, v4
	v_mul_f32_e32 v5, 0x43800000, v95
	v_mul_f32_e32 v6, 0x43800000, v111
	v_med3_f32 v5, v5, s85, v252
	v_med3_f32 v6, v6, s85, v252
	v_cvt_pk_fp8_f32 v3, v5, v6 op_sel:[0,0,1]
	v_mul_f32_e32 v4, 0x43800000, v27
	v_mul_f32_e32 v5, 0x43800000, v39
	v_med3_f32 v14, v4, s85, v252
	v_med3_f32 v5, v5, s85, v252
	v_mov_b32_e32 v4, v155
	v_cvt_pk_fp8_f32 v4, v14, v5
	v_mul_f32_e32 v6, 0x43800000, v63
	v_mul_f32_e32 v10, 0x43800000, v75
	v_med3_f32 v6, v6, s85, v252
	v_med3_f32 v10, v10, s85, v252
	v_cvt_pk_fp8_f32 v4, v6, v10 op_sel:[0,0,1]
	v_mul_f32_e32 v5, 0x43800000, v7
	v_mul_f32_e32 v6, 0x43800000, v11
	v_med3_f32 v11, v5, s85, v252
	v_med3_f32 v6, v6, s85, v252
	v_mov_b32_e32 v5, v155
	v_cvt_pk_fp8_f32 v5, v11, v6
	v_mul_f32_e32 v7, 0x43800000, v31
	v_mul_f32_e32 v10, 0x43800000, v43
	v_med3_f32 v7, v7, s85, v252
	v_med3_f32 v10, v10, s85, v252
	v_cvt_pk_fp8_f32 v5, v7, v10 op_sel:[0,0,1]
	ds_write_b128 v164, v[2:5] offset:35088
	v_mul_f32_e32 v2, 0x43800000, v92
	v_mul_f32_e32 v3, 0x43800000, v108
	v_med3_f32 v6, v2, s85, v252
	v_med3_f32 v3, v3, s85, v252
	v_mov_b32_e32 v2, v155
	v_cvt_pk_fp8_f32 v2, v6, v3
	v_mul_f32_e32 v4, 0x43800000, v124
	v_mul_f32_e32 v5, 0x43800000, v128
	v_med3_f32 v4, v4, s85, v252
	v_med3_f32 v5, v5, s85, v252
	v_cvt_pk_fp8_f32 v2, v4, v5 op_sel:[0,0,1]
	v_mul_f32_e32 v3, 0x43800000, v60
	v_mul_f32_e32 v4, 0x43800000, v72
	v_med3_f32 v7, v3, s85, v252
	v_med3_f32 v4, v4, s85, v252
	v_mov_b32_e32 v3, v155
	v_cvt_pk_fp8_f32 v3, v7, v4
	v_mul_f32_e32 v5, 0x43800000, v96
	v_mul_f32_e32 v6, 0x43800000, v112
	v_med3_f32 v5, v5, s85, v252
	v_med3_f32 v6, v6, s85, v252
	v_cvt_pk_fp8_f32 v3, v5, v6 op_sel:[0,0,1]
	v_mul_f32_e32 v4, 0x43800000, v28
	v_mul_f32_e32 v5, 0x43800000, v40
	v_med3_f32 v10, v4, s85, v252
	v_med3_f32 v5, v5, s85, v252
	v_mov_b32_e32 v4, v155
	v_cvt_pk_fp8_f32 v4, v10, v5
	v_mul_f32_e32 v6, 0x43800000, v64
	v_mul_f32_e32 v7, 0x43800000, v76
	v_med3_f32 v6, v6, s85, v252
	v_med3_f32 v7, v7, s85, v252
	v_cvt_pk_fp8_f32 v4, v6, v7 op_sel:[0,0,1]
	v_mul_f32_e32 v5, 0x43800000, v8
	v_mul_f32_e32 v6, 0x43800000, v12
	v_med3_f32 v10, v5, s85, v252
	v_med3_f32 v6, v6, s85, v252
	v_mov_b32_e32 v5, v155
	v_cvt_pk_fp8_f32 v5, v10, v6
	v_mul_f32_e32 v7, 0x43800000, v32
	v_mul_f32_e32 v8, 0x43800000, v44
	v_med3_f32 v7, v7, s85, v252
	v_med3_f32 v8, v8, s85, v252
	v_cvt_pk_fp8_f32 v5, v7, v8 op_sel:[0,0,1]
	ds_write_b128 v164, v[2:5] offset:35360
	v_mul_f32_e32 v2, 0x43800000, v93
	v_mul_f32_e32 v3, 0x43800000, v109
	v_med3_f32 v6, v2, s85, v252
	v_med3_f32 v3, v3, s85, v252
	v_mov_b32_e32 v2, v155
	v_cvt_pk_fp8_f32 v2, v6, v3
	v_mul_f32_e32 v4, 0x43800000, v125
	v_mul_f32_e32 v5, 0x43800000, v129
	v_med3_f32 v4, v4, s85, v252
	v_med3_f32 v5, v5, s85, v252
	v_cvt_pk_fp8_f32 v2, v4, v5 op_sel:[0,0,1]
	v_mul_f32_e32 v3, 0x43800000, v61
	v_mul_f32_e32 v4, 0x43800000, v73
	v_med3_f32 v7, v3, s85, v252
	v_med3_f32 v4, v4, s85, v252
	v_mov_b32_e32 v3, v155
	v_cvt_pk_fp8_f32 v3, v7, v4
	v_mul_f32_e32 v5, 0x43800000, v97
	v_mul_f32_e32 v6, 0x43800000, v113
	v_med3_f32 v5, v5, s85, v252
	v_med3_f32 v6, v6, s85, v252
	v_cvt_pk_fp8_f32 v3, v5, v6 op_sel:[0,0,1]
	v_mul_f32_e32 v4, 0x43800000, v29
	v_mul_f32_e32 v5, 0x43800000, v41
	v_med3_f32 v8, v4, s85, v252
	v_med3_f32 v5, v5, s85, v252
	v_mov_b32_e32 v4, v155
	v_cvt_pk_fp8_f32 v4, v8, v5
	v_mul_f32_e32 v6, 0x43800000, v65
	v_mul_f32_e32 v7, 0x43800000, v77
	v_med3_f32 v6, v6, s85, v252
	v_med3_f32 v7, v7, s85, v252
	v_cvt_pk_fp8_f32 v4, v6, v7 op_sel:[0,0,1]
	v_mul_f32_e32 v5, 0x43800000, v9
	v_mul_f32_e32 v6, 0x43800000, v13
	v_med3_f32 v9, v5, s85, v252
	v_med3_f32 v6, v6, s85, v252
	v_mov_b32_e32 v5, v155
	v_cvt_pk_fp8_f32 v5, v9, v6
	v_mul_f32_e32 v7, 0x43800000, v33
	v_mul_f32_e32 v8, 0x43800000, v45
	v_med3_f32 v7, v7, s85, v252
	v_med3_f32 v8, v8, s85, v252
	v_cvt_pk_fp8_f32 v5, v7, v8 op_sel:[0,0,1]
	ds_write_b128 v164, v[2:5] offset:35632
	s_waitcnt lgkmcnt(0)
	s_barrier
	ds_read_b128 v[2:5], v142 offset:34816
	s_waitcnt lgkmcnt(0)
	global_store_dwordx4 v[144:145], v[2:5], off offset:1792 nt
	ds_read_b128 v[2:5], v146 offset:34816
	s_waitcnt lgkmcnt(0)
	global_store_dwordx4 v[148:149], v[2:5], off offset:1792 nt
	ds_read_b128 v[2:5], v150 offset:34816
	s_waitcnt lgkmcnt(0)
	global_store_dwordx4 v[152:153], v[2:5], off offset:1792 nt
	ds_read_b128 v[2:5], v158 offset:34816
	s_waitcnt lgkmcnt(0)
	global_store_dwordx4 v[160:161], v[2:5], off offset:1792 nt
	s_barrier

.LBB0_273:
	v_readlane_b32 s78, v254, 57
	v_readlane_b32 s16, v254, 63
	v_readlane_b32 s66, v254, 61
	s_bitcmp1_b32 s3, 5
	v_readlane_b32 s79, v254, 58
	v_readlane_b32 s64, v254, 53
	v_readlane_b32 s77, v254, 54
	v_readlane_b32 s17, v255, 0
	v_readlane_b32 s67, v254, 62
	v_and_b32_e32 v252, 63, v0
	s_cbranch_scc0 .LBB0_279
	s_cmpk_gt_i32 s4, 0x3ff
	s_mov_b64 s[8:9], -1
	s_cbranch_scc0 .LBB0_276
	s_add_i32 s0, s4, 0xfffffc00
	s_lshr_b32 s0, s0, 4
	s_mov_b32 s1, 0
	v_readlane_b32 s8, v254, 4
	s_lshl_b64 s[2:3], s[0:1], 24
	v_readlane_b32 s14, v254, 10
	v_readlane_b32 s15, v254, 11
	s_add_u32 s2, s14, s2
	s_addc_u32 s3, s15, s3
	s_lshl_b32 s6, s4, 7
	s_and_b32 s6, s6, 0x780
	s_lshl_b32 s7, s6, 2
	s_add_u32 s2, s2, s7
	s_addc_u32 s3, s3, 0
	s_lshl_b64 s[0:1], s[0:1], 22
	s_lshl_b32 s6, s6, 11
	v_readlane_b32 s7, v255, 1
	s_add_u32 s0, s7, s0
	v_readlane_b32 s7, v255, 3
	v_mov_b32_e32 v134, v0
	s_addc_u32 s1, s7, s1
	v_readlane_b32 s9, v254, 5
	v_readfirstlane_b32 s5, v134
	s_add_u32 s8, s0, s6
	s_addc_u32 s9, s1, 0
	s_ashr_i32 s0, s5, 1
	v_lshrrev_b32_e32 v1, 1, v134
	s_andn2_b32 s0, s0, 31
	v_and_b32_e32 v135, 16, v1
	v_or_b32_e32 v2, s0, v135
	v_ashrrev_i32_e32 v3, 31, v2
	v_lshlrev_b32_e32 v1, 2, v134
	v_lshlrev_b64 v[2:3], 13, v[2:3]
	v_and_b32_e32 v140, 0x7c, v1
	v_lshl_add_u64 v[2:3], s[2:3], 0, v[2:3]
	s_waitcnt lgkmcnt(0)
	v_lshlrev_b32_e32 v4, 2, v140
	v_mov_b32_e32 v5, 0
	v_lshl_add_u64 v[2:3], v[2:3], 0, v[4:5]
	s_movk_i32 s1, 0x2000
	v_add_co_u32_e32 v6, vcc, s1, v2
	s_movk_i32 s1, 0x4000
	s_nop 0
	v_addc_co_u32_e32 v7, vcc, 0, v3, vcc
	global_load_dwordx4 v[34:37], v[2:3], off sc0 nt
	global_load_dwordx4 v[46:49], v[6:7], off sc0 nt
	v_add_co_u32_e32 v6, vcc, s1, v2
	s_movk_i32 s1, 0x6000
	s_nop 0
	v_addc_co_u32_e32 v7, vcc, 0, v3, vcc
	v_add_co_u32_e32 v8, vcc, s1, v2
	s_mov_b32 s1, 0x8000
	s_nop 0
	v_addc_co_u32_e32 v9, vcc, 0, v3, vcc
	global_load_dwordx4 v[62:65], v[6:7], off sc0 nt
	global_load_dwordx4 v[54:57], v[8:9], off sc0 nt
	v_add_co_u32_e32 v6, vcc, s1, v2
	s_mov_b32 s1, 0xa000
	s_nop 0
	v_addc_co_u32_e32 v7, vcc, 0, v3, vcc
	v_add_co_u32_e32 v8, vcc, s1, v2
	s_mov_b32 s1, 0xc000
	s_nop 0
	v_addc_co_u32_e32 v9, vcc, 0, v3, vcc
	global_load_dwordx4 v[66:69], v[6:7], off sc0 nt
	global_load_dwordx4 v[78:81], v[8:9], off sc0 nt
	v_add_co_u32_e32 v6, vcc, s1, v2
	s_mov_b32 s1, 0xe000
	s_nop 0
	v_addc_co_u32_e32 v7, vcc, 0, v3, vcc
	v_add_co_u32_e32 v8, vcc, s1, v2
	s_mov_b32 s1, 0x10000
	s_nop 0
	v_addc_co_u32_e32 v9, vcc, 0, v3, vcc
	global_load_dwordx4 v[94:97], v[6:7], off sc0 nt
	global_load_dwordx4 v[86:89], v[8:9], off sc0 nt
	v_add_co_u32_e32 v6, vcc, s1, v2
	s_mov_b32 s1, 0x12000
	s_nop 0
	v_addc_co_u32_e32 v7, vcc, 0, v3, vcc
	v_add_co_u32_e32 v8, vcc, s1, v2
	s_mov_b32 s1, 0x14000
	s_nop 0
	v_addc_co_u32_e32 v9, vcc, 0, v3, vcc
	global_load_dwordx4 v[98:101], v[6:7], off sc0 nt
	global_load_dwordx4 v[106:109], v[8:9], off sc0 nt
	v_add_co_u32_e32 v6, vcc, s1, v2
	s_mov_b32 s1, 0x16000
	s_nop 0
	v_addc_co_u32_e32 v7, vcc, 0, v3, vcc
	v_add_co_u32_e32 v8, vcc, s1, v2
	s_mov_b32 s1, 0x18000
	s_nop 0
	v_addc_co_u32_e32 v9, vcc, 0, v3, vcc
	global_load_dwordx4 v[114:117], v[6:7], off sc0 nt
	global_load_dwordx4 v[110:113], v[8:9], off sc0 nt
	v_add_co_u32_e32 v6, vcc, s1, v2
	s_mov_b32 s1, 0x1a000
	s_nop 0
	v_addc_co_u32_e32 v7, vcc, 0, v3, vcc
	v_add_co_u32_e32 v8, vcc, s1, v2
	s_mov_b32 s1, 0x1c000
	s_nop 0
	v_addc_co_u32_e32 v9, vcc, 0, v3, vcc
	global_load_dwordx4 v[118:121], v[6:7], off sc0 nt
	global_load_dwordx4 v[122:125], v[8:9], off sc0 nt
	v_add_co_u32_e32 v6, vcc, s1, v2
	s_mov_b32 s1, 0x1e000
	s_nop 0
	v_addc_co_u32_e32 v7, vcc, 0, v3, vcc
	v_add_co_u32_e32 v8, vcc, s1, v2
	s_mov_b32 s1, 0x200000
	s_nop 0
	v_addc_co_u32_e32 v9, vcc, 0, v3, vcc
	global_load_dwordx4 v[130:133], v[6:7], off sc0 nt
	global_load_dwordx4 v[126:129], v[8:9], off sc0 nt
	v_add_co_u32_e32 v6, vcc, s1, v2
	s_mov_b32 s1, 0x202000
	s_nop 0
	v_addc_co_u32_e32 v7, vcc, 0, v3, vcc
	v_add_co_u32_e32 v10, vcc, s1, v2
	s_mov_b32 s1, 0x204000
	s_nop 0
	v_addc_co_u32_e32 v11, vcc, 0, v3, vcc
	v_add_co_u32_e32 v14, vcc, s1, v2
	s_mov_b32 s1, 0x206000
	s_nop 0
	v_addc_co_u32_e32 v15, vcc, 0, v3, vcc
	v_add_co_u32_e32 v16, vcc, s1, v2
	s_mov_b32 s1, 0x208000
	s_nop 0
	v_addc_co_u32_e32 v17, vcc, 0, v3, vcc
	v_add_co_u32_e32 v22, vcc, s1, v2
	s_mov_b32 s1, 0x20a000
	s_nop 0
	v_addc_co_u32_e32 v23, vcc, 0, v3, vcc
	v_add_co_u32_e32 v26, vcc, s1, v2
	s_mov_b32 s1, 0x20c000
	s_nop 0
	v_addc_co_u32_e32 v27, vcc, 0, v3, vcc
	v_add_co_u32_e32 v30, vcc, s1, v2
	s_mov_b32 s1, 0x20e000
	s_nop 0
	v_addc_co_u32_e32 v31, vcc, 0, v3, vcc
	v_add_co_u32_e32 v32, vcc, s1, v2
	s_mov_b32 s1, 0x210000
	s_nop 0
	v_addc_co_u32_e32 v33, vcc, 0, v3, vcc
	v_add_co_u32_e32 v42, vcc, s1, v2
	s_mov_b32 s1, 0x212000
	s_nop 0
	v_addc_co_u32_e32 v43, vcc, 0, v3, vcc
	v_add_co_u32_e32 v50, vcc, s1, v2
	s_mov_b32 s1, 0x214000
	s_nop 0
	v_addc_co_u32_e32 v51, vcc, 0, v3, vcc
	v_add_co_u32_e32 v58, vcc, s1, v2
	s_mov_b32 s1, 0x216000
	s_nop 0
	v_addc_co_u32_e32 v59, vcc, 0, v3, vcc
	v_add_co_u32_e32 v60, vcc, s1, v2
	s_mov_b32 s1, 0x218000
	s_nop 0
	v_addc_co_u32_e32 v61, vcc, 0, v3, vcc
	v_add_co_u32_e32 v74, vcc, s1, v2
	s_mov_b32 s1, 0x21a000
	s_nop 0
	v_addc_co_u32_e32 v75, vcc, 0, v3, vcc
	v_add_co_u32_e32 v82, vcc, s1, v2
	s_mov_b32 s1, 0x21c000
	s_nop 0
	v_addc_co_u32_e32 v83, vcc, 0, v3, vcc
	v_add_co_u32_e32 v90, vcc, s1, v2
	s_mov_b32 s1, 0x21e000
	s_nop 0
	v_addc_co_u32_e32 v91, vcc, 0, v3, vcc
	v_add_co_u32_e32 v92, vcc, s1, v2
	global_load_dwordx4 v[6:9], v[6:7], off sc0 nt
	s_nop 0
	global_load_dwordx4 v[10:13], v[10:11], off sc0 nt
	v_addc_co_u32_e32 v93, vcc, 0, v3, vcc
	global_load_dwordx4 v[18:21], v[14:15], off sc0 nt
	s_nop 0
	global_load_dwordx4 v[14:17], v[16:17], off sc0 nt
	s_nop 0
	global_load_dwordx4 v[22:25], v[22:23], off sc0 nt
	s_nop 0
	global_load_dwordx4 v[26:29], v[26:27], off sc0 nt
	s_nop 0
	global_load_dwordx4 v[38:41], v[30:31], off sc0 nt
	s_nop 0
	global_load_dwordx4 v[30:33], v[32:33], off sc0 nt
	s_nop 0
	global_load_dwordx4 v[42:45], v[42:43], off sc0 nt
	s_nop 0
	global_load_dwordx4 v[50:53], v[50:51], off sc0 nt
	s_nop 0
	global_load_dwordx4 v[70:73], v[58:59], off sc0 nt
	s_nop 0
	global_load_dwordx4 v[58:61], v[60:61], off sc0 nt
	s_nop 0
	global_load_dwordx4 v[74:77], v[74:75], off sc0 nt
	s_nop 0
	global_load_dwordx4 v[82:85], v[82:83], off sc0 nt
	s_nop 0
	global_load_dwordx4 v[102:105], v[90:91], off sc0 nt
	s_nop 0
	global_load_dwordx4 v[90:93], v[92:93], off sc0 nt
	v_readlane_b32 s10, v254, 6
	v_readlane_b32 s11, v254, 7
	v_readlane_b32 s12, v254, 8
	v_readlane_b32 s13, v254, 9
	s_add_i32 s2, s0, 0
	s_waitcnt vmcnt(0)
	v_mul_f32_e32 v4, 0x43800000, v34
	v_mul_f32_e32 v34, 0x43800000, v46
	s_mov_b32 s0, 0xc3e00000
	v_mov_b32_e32 v1, 0x43e00000
	v_med3_f32 v4, v4, s0, v1
	v_med3_f32 v34, v34, s0, v1
	v_mov_b32_e32 v136, v5
	v_cvt_pk_fp8_f32 v136, v4, v34
	v_mul_f32_e32 v46, 0x43800000, v62
	v_mul_f32_e32 v4, 0x43800000, v54
	v_med3_f32 v34, v46, s0, v1
	v_med3_f32 v4, v4, s0, v1
	v_cvt_pk_fp8_f32 v136, v34, v4 op_sel:[0,0,1]
	v_mul_f32_e32 v4, 0x43800000, v66
	v_mul_f32_e32 v34, 0x43800000, v78
	v_med3_f32 v4, v4, s0, v1
	v_med3_f32 v34, v34, s0, v1
	v_mov_b32_e32 v137, v5
	v_cvt_pk_fp8_f32 v137, v4, v34
	v_mul_f32_e32 v46, 0x43800000, v94
	v_mul_f32_e32 v4, 0x43800000, v86
	v_med3_f32 v34, v46, s0, v1
	v_med3_f32 v4, v4, s0, v1
	v_cvt_pk_fp8_f32 v137, v34, v4 op_sel:[0,0,1]
	v_mul_f32_e32 v4, 0x43800000, v98
	v_mul_f32_e32 v34, 0x43800000, v106
	v_med3_f32 v4, v4, s0, v1
	v_med3_f32 v34, v34, s0, v1
	v_mov_b32_e32 v138, v5
	v_cvt_pk_fp8_f32 v138, v4, v34
	v_mul_f32_e32 v46, 0x43800000, v114
	v_mul_f32_e32 v4, 0x43800000, v110
	v_med3_f32 v34, v46, s0, v1
	v_med3_f32 v4, v4, s0, v1
	v_cvt_pk_fp8_f32 v138, v34, v4 op_sel:[0,0,1]
	v_mul_f32_e32 v4, 0x43800000, v118
	v_mul_f32_e32 v34, 0x43800000, v122
	v_med3_f32 v4, v4, s0, v1
	v_med3_f32 v34, v34, s0, v1
	v_mov_b32_e32 v139, v5
	v_cvt_pk_fp8_f32 v139, v4, v34
	v_mul_f32_e32 v46, 0x43800000, v130
	v_mul_f32_e32 v4, 0x43800000, v126
	v_med3_f32 v34, v46, s0, v1
	v_med3_f32 v4, v4, s0, v1
	v_cvt_pk_fp8_f32 v139, v34, v4 op_sel:[0,0,1]
	v_mul_u32_u24_e32 v4, 0x110, v140
	v_add3_u32 v166, s2, v135, v4
	v_mul_f32_e32 v4, 0x43800000, v35
	v_mul_f32_e32 v34, 0x43800000, v47
	v_med3_f32 v4, v4, s0, v1
	v_med3_f32 v34, v34, s0, v1
	v_mov_b32_e32 v140, v5
	v_cvt_pk_fp8_f32 v140, v4, v34
	v_mul_f32_e32 v35, 0x43800000, v63
	v_mul_f32_e32 v4, 0x43800000, v55
	v_med3_f32 v34, v35, s0, v1
	v_med3_f32 v4, v4, s0, v1
	v_cvt_pk_fp8_f32 v140, v34, v4 op_sel:[0,0,1]
	v_mul_f32_e32 v4, 0x43800000, v67
	v_mul_f32_e32 v34, 0x43800000, v79
	v_med3_f32 v4, v4, s0, v1
	v_med3_f32 v34, v34, s0, v1
	v_mov_b32_e32 v141, v5
	v_cvt_pk_fp8_f32 v141, v4, v34
	v_mul_f32_e32 v35, 0x43800000, v95
	v_mul_f32_e32 v4, 0x43800000, v87
	v_med3_f32 v34, v35, s0, v1
	v_med3_f32 v4, v4, s0, v1
	v_cvt_pk_fp8_f32 v141, v34, v4 op_sel:[0,0,1]
	v_mul_f32_e32 v4, 0x43800000, v99
	v_mul_f32_e32 v34, 0x43800000, v107
	v_med3_f32 v4, v4, s0, v1
	v_med3_f32 v34, v34, s0, v1
	v_mov_b32_e32 v142, v5
	v_cvt_pk_fp8_f32 v142, v4, v34
	v_mul_f32_e32 v35, 0x43800000, v115
	v_mul_f32_e32 v4, 0x43800000, v111
	v_med3_f32 v34, v35, s0, v1
	v_med3_f32 v4, v4, s0, v1
	v_cvt_pk_fp8_f32 v142, v34, v4 op_sel:[0,0,1]
	v_mul_f32_e32 v4, 0x43800000, v119
	v_mul_f32_e32 v34, 0x43800000, v123
	v_med3_f32 v4, v4, s0, v1
	v_med3_f32 v34, v34, s0, v1
	v_mov_b32_e32 v143, v5
	v_cvt_pk_fp8_f32 v143, v4, v34
	v_mul_f32_e32 v35, 0x43800000, v131
	v_mul_f32_e32 v4, 0x43800000, v127
	v_med3_f32 v34, v35, s0, v1
	v_med3_f32 v4, v4, s0, v1
	v_cvt_pk_fp8_f32 v143, v34, v4 op_sel:[0,0,1]
	v_mul_f32_e32 v4, 0x43800000, v36
	v_mul_f32_e32 v34, 0x43800000, v48
	v_med3_f32 v4, v4, s0, v1
	v_med3_f32 v34, v34, s0, v1
	v_mov_b32_e32 v144, v5
	v_cvt_pk_fp8_f32 v144, v4, v34
	v_mul_f32_e32 v35, 0x43800000, v64
	v_mul_f32_e32 v4, 0x43800000, v56
	v_med3_f32 v34, v35, s0, v1
	v_med3_f32 v4, v4, s0, v1
	v_cvt_pk_fp8_f32 v144, v34, v4 op_sel:[0,0,1]
	v_mul_f32_e32 v4, 0x43800000, v68
	v_mul_f32_e32 v34, 0x43800000, v80
	v_med3_f32 v4, v4, s0, v1
	v_med3_f32 v34, v34, s0, v1
	v_mov_b32_e32 v145, v5
	v_cvt_pk_fp8_f32 v145, v4, v34
	v_mul_f32_e32 v35, 0x43800000, v96
	v_mul_f32_e32 v4, 0x43800000, v88
	v_med3_f32 v34, v35, s0, v1
	v_med3_f32 v4, v4, s0, v1
	v_cvt_pk_fp8_f32 v145, v34, v4 op_sel:[0,0,1]
	v_mul_f32_e32 v4, 0x43800000, v100
	v_mul_f32_e32 v34, 0x43800000, v108
	v_med3_f32 v4, v4, s0, v1
	v_med3_f32 v34, v34, s0, v1
	v_mov_b32_e32 v146, v5
	v_cvt_pk_fp8_f32 v146, v4, v34
	v_mul_f32_e32 v35, 0x43800000, v116
	v_mul_f32_e32 v4, 0x43800000, v112
	v_med3_f32 v34, v35, s0, v1
	v_med3_f32 v4, v4, s0, v1
	v_cvt_pk_fp8_f32 v146, v34, v4 op_sel:[0,0,1]
	v_mul_f32_e32 v4, 0x43800000, v120
	v_mul_f32_e32 v34, 0x43800000, v124
	v_med3_f32 v4, v4, s0, v1
	v_med3_f32 v34, v34, s0, v1
	v_mov_b32_e32 v147, v5
	v_cvt_pk_fp8_f32 v147, v4, v34
	v_mul_f32_e32 v35, 0x43800000, v132
	v_mul_f32_e32 v4, 0x43800000, v128
	v_med3_f32 v34, v35, s0, v1
	v_med3_f32 v4, v4, s0, v1
	v_cvt_pk_fp8_f32 v147, v34, v4 op_sel:[0,0,1]
	v_mul_f32_e32 v4, 0x43800000, v37
	v_mul_f32_e32 v34, 0x43800000, v49
	v_med3_f32 v4, v4, s0, v1
	v_med3_f32 v36, v34, s0, v1
	v_mov_b32_e32 v34, v5
	v_cvt_pk_fp8_f32 v34, v4, v36
	v_mul_f32_e32 v35, 0x43800000, v65
	v_mul_f32_e32 v4, 0x43800000, v57
	v_med3_f32 v35, v35, s0, v1
	v_med3_f32 v4, v4, s0, v1
	v_cvt_pk_fp8_f32 v34, v35, v4 op_sel:[0,0,1]
	v_mul_f32_e32 v4, 0x43800000, v69
	v_mul_f32_e32 v35, 0x43800000, v81
	v_med3_f32 v4, v4, s0, v1
	v_med3_f32 v37, v35, s0, v1
	v_mov_b32_e32 v35, v5
	v_cvt_pk_fp8_f32 v35, v4, v37
	v_mul_f32_e32 v36, 0x43800000, v97
	v_mul_f32_e32 v4, 0x43800000, v89
	v_med3_f32 v36, v36, s0, v1
	v_med3_f32 v4, v4, s0, v1
	v_cvt_pk_fp8_f32 v35, v36, v4 op_sel:[0,0,1]
	v_mul_f32_e32 v4, 0x43800000, v101
	v_mul_f32_e32 v36, 0x43800000, v109
	v_med3_f32 v4, v4, s0, v1
	v_med3_f32 v46, v36, s0, v1
	v_mov_b32_e32 v36, v5
	v_cvt_pk_fp8_f32 v36, v4, v46
	v_mul_f32_e32 v37, 0x43800000, v117
	v_mul_f32_e32 v4, 0x43800000, v113
	v_med3_f32 v37, v37, s0, v1
	v_med3_f32 v4, v4, s0, v1
	v_cvt_pk_fp8_f32 v36, v37, v4 op_sel:[0,0,1]
	v_mul_f32_e32 v4, 0x43800000, v121
	v_mul_f32_e32 v37, 0x43800000, v125
	v_med3_f32 v4, v4, s0, v1
	v_med3_f32 v47, v37, s0, v1
	v_mov_b32_e32 v37, v5
	v_cvt_pk_fp8_f32 v37, v4, v47
	v_mul_f32_e32 v46, 0x43800000, v133
	v_mul_f32_e32 v4, 0x43800000, v129
	v_med3_f32 v46, v46, s0, v1
	v_med3_f32 v4, v4, s0, v1
	v_cvt_pk_fp8_f32 v37, v46, v4 op_sel:[0,0,1]
	ds_write_b128 v166, v[136:139]
	ds_write_b128 v166, v[140:143] offset:272
	ds_write_b128 v166, v[144:147] offset:544
	ds_write_b128 v166, v[34:37] offset:816
	v_add_u32_e32 v34, 0x200, v134
	v_ashrrev_i32_e32 v140, 4, v34
	v_add_u32_e32 v34, 0x400, v134
	v_ashrrev_i32_e32 v144, 4, v34
	v_add_u32_e32 v34, 0x600, v134
	v_ashrrev_i32_e32 v136, 4, v134
	v_ashrrev_i32_e32 v148, 4, v34
	v_lshlrev_b32_e32 v4, 4, v134
	v_ashrrev_i32_e32 v137, 31, v136
	v_ashrrev_i32_e32 v141, 31, v140
	v_ashrrev_i32_e32 v145, 31, v144
	v_ashrrev_i32_e32 v149, 31, v148
	s_movk_i32 s1, 0x110
	s_waitcnt lgkmcnt(0)
	s_barrier
	v_and_b32_e32 v4, 0xf0, v4
	v_lshlrev_b64 v[138:139], 11, v[136:137]
	v_lshlrev_b64 v[142:143], 11, v[140:141]
	v_lshlrev_b64 v[146:147], 11, v[144:145]
	v_lshlrev_b64 v[164:165], 11, v[148:149]
	s_mov_b32 s2, 0x400000
	v_add_co_u32_e32 v34, vcc, s2, v2
	s_mov_b32 s2, 0x402000
	s_nop 0
	v_addc_co_u32_e32 v35, vcc, 0, v3, vcc
	v_add_co_u32_e32 v46, vcc, s2, v2
	s_mov_b32 s2, 0x404000
	s_nop 0
	v_addc_co_u32_e32 v47, vcc, 0, v3, vcc
	v_add_co_u32_e32 v54, vcc, s2, v2
	s_mov_b32 s2, 0x406000
	s_nop 0
	v_addc_co_u32_e32 v55, vcc, 0, v3, vcc
	v_add_co_u32_e32 v56, vcc, s2, v2
	s_mov_b32 s2, 0x408000
	s_nop 0
	v_addc_co_u32_e32 v57, vcc, 0, v3, vcc
	v_add_co_u32_e32 v66, vcc, s2, v2
	s_mov_b32 s2, 0x40a000
	s_nop 0
	v_addc_co_u32_e32 v67, vcc, 0, v3, vcc
	v_add_co_u32_e32 v78, vcc, s2, v2
	s_mov_b32 s2, 0x40c000
	s_nop 0
	v_addc_co_u32_e32 v79, vcc, 0, v3, vcc
	v_add_co_u32_e32 v86, vcc, s2, v2
	s_mov_b32 s2, 0x40e000
	s_nop 0
	v_addc_co_u32_e32 v87, vcc, 0, v3, vcc
	v_add_co_u32_e32 v88, vcc, s2, v2
	s_mov_b32 s2, 0x410000
	s_nop 0
	v_addc_co_u32_e32 v89, vcc, 0, v3, vcc
	v_add_co_u32_e32 v98, vcc, s2, v2
	s_mov_b32 s2, 0x412000
	s_nop 0
	v_addc_co_u32_e32 v99, vcc, 0, v3, vcc
	v_add_co_u32_e32 v106, vcc, s2, v2
	s_mov_b32 s2, 0x414000
	s_nop 0
	v_addc_co_u32_e32 v107, vcc, 0, v3, vcc
	v_add_co_u32_e32 v110, vcc, s2, v2
	s_mov_b32 s2, 0x416000
	s_nop 0
	v_addc_co_u32_e32 v111, vcc, 0, v3, vcc
	v_add_co_u32_e32 v112, vcc, s2, v2
	s_mov_b32 s2, 0x418000
	s_nop 0
	v_addc_co_u32_e32 v113, vcc, 0, v3, vcc
	v_add_co_u32_e32 v118, vcc, s2, v2
	s_mov_b32 s2, 0x41a000
	s_nop 0
	v_addc_co_u32_e32 v119, vcc, 0, v3, vcc
	v_add_co_u32_e32 v122, vcc, s2, v2
	s_mov_b32 s2, 0x41c000
	s_nop 0
	v_addc_co_u32_e32 v123, vcc, 0, v3, vcc
	v_add_co_u32_e32 v126, vcc, s2, v2
	s_mov_b32 s2, 0x41e000
	s_nop 0
	v_addc_co_u32_e32 v127, vcc, 0, v3, vcc
	v_add_co_u32_e32 v128, vcc, s2, v2
	global_load_dwordx4 v[34:37], v[34:35], off sc0 nt
	s_nop 0
	global_load_dwordx4 v[46:49], v[46:47], off sc0 nt
	v_addc_co_u32_e32 v129, vcc, 0, v3, vcc
	global_load_dwordx4 v[62:65], v[54:55], off sc0 nt
	s_nop 0
	global_load_dwordx4 v[54:57], v[56:57], off sc0 nt
	s_nop 0
	global_load_dwordx4 v[66:69], v[66:67], off sc0 nt
	s_nop 0
	global_load_dwordx4 v[78:81], v[78:79], off sc0 nt
	s_nop 0
	global_load_dwordx4 v[94:97], v[86:87], off sc0 nt
	s_nop 0
	global_load_dwordx4 v[86:89], v[88:89], off sc0 nt
	s_nop 0
	global_load_dwordx4 v[98:101], v[98:99], off sc0 nt
	s_nop 0
	global_load_dwordx4 v[106:109], v[106:107], off sc0 nt
	s_nop 0
	global_load_dwordx4 v[114:117], v[110:111], off sc0 nt
	s_nop 0
	global_load_dwordx4 v[110:113], v[112:113], off sc0 nt
	s_nop 0
	global_load_dwordx4 v[118:121], v[118:119], off sc0 nt
	s_nop 0
	global_load_dwordx4 v[122:125], v[122:123], off sc0 nt
	s_nop 0
	global_load_dwordx4 v[130:133], v[126:127], off sc0 nt
	s_nop 0
	global_load_dwordx4 v[126:129], v[128:129], off sc0 nt
	v_add_u32_e32 v160, 0, v4
	v_mad_u64_u32 v[154:155], s[2:3], v136, s1, v[160:161]
	ds_read_b128 v[134:137], v154
	v_lshl_add_u64 v[168:169], s[8:9], 0, v[4:5]
	v_lshl_add_u64 v[150:151], v[168:169], 0, v[138:139]
	v_mad_u64_u32 v[156:157], s[2:3], v140, s1, v[160:161]
	v_mad_u64_u32 v[158:159], s[2:3], v144, s1, v[160:161]
	v_mad_u64_u32 v[162:163], s[2:3], v148, s1, v[160:161]
	ds_read_b128 v[138:141], v156
	s_waitcnt lgkmcnt(1)
	global_store_dwordx4 v[150:151], v[134:137], off nt
	v_lshl_add_u64 v[152:153], v[168:169], 0, v[142:143]
	ds_read_b128 v[134:137], v158
	ds_read_b128 v[142:145], v162
	v_lshl_add_u64 v[160:161], v[168:169], 0, v[146:147]
	v_lshl_add_u64 v[164:165], v[168:169], 0, v[164:165]
	s_waitcnt lgkmcnt(2)
	global_store_dwordx4 v[152:153], v[138:141], off nt
	s_waitcnt lgkmcnt(1)
	global_store_dwordx4 v[160:161], v[134:137], off nt
	s_waitcnt lgkmcnt(0)
	global_store_dwordx4 v[164:165], v[142:145], off nt
	v_mul_f32_e32 v4, 0x43800000, v6
	v_mul_f32_e32 v6, 0x43800000, v10
	v_med3_f32 v4, v4, s0, v1
	v_med3_f32 v6, v6, s0, v1
	v_mov_b32_e32 v134, v5
	v_cvt_pk_fp8_f32 v134, v4, v6
	v_mul_f32_e32 v10, 0x43800000, v18
	v_mul_f32_e32 v4, 0x43800000, v14
	v_med3_f32 v6, v10, s0, v1
	v_med3_f32 v4, v4, s0, v1
	v_cvt_pk_fp8_f32 v134, v6, v4 op_sel:[0,0,1]
	v_mul_f32_e32 v4, 0x43800000, v22
	v_mul_f32_e32 v6, 0x43800000, v26
	v_med3_f32 v4, v4, s0, v1
	v_med3_f32 v6, v6, s0, v1
	v_mov_b32_e32 v135, v5
	v_cvt_pk_fp8_f32 v135, v4, v6
	v_mul_f32_e32 v10, 0x43800000, v38
	v_mul_f32_e32 v4, 0x43800000, v30
	v_med3_f32 v6, v10, s0, v1
	v_med3_f32 v4, v4, s0, v1
	v_cvt_pk_fp8_f32 v135, v6, v4 op_sel:[0,0,1]
	v_mul_f32_e32 v4, 0x43800000, v42
	v_mul_f32_e32 v6, 0x43800000, v50
	v_med3_f32 v4, v4, s0, v1
	v_med3_f32 v6, v6, s0, v1
	v_mov_b32_e32 v136, v5
	v_cvt_pk_fp8_f32 v136, v4, v6
	v_mul_f32_e32 v10, 0x43800000, v70
	v_mul_f32_e32 v4, 0x43800000, v58
	v_med3_f32 v6, v10, s0, v1
	v_med3_f32 v4, v4, s0, v1
	v_cvt_pk_fp8_f32 v136, v6, v4 op_sel:[0,0,1]
	v_mul_f32_e32 v4, 0x43800000, v74
	v_mul_f32_e32 v6, 0x43800000, v82
	v_med3_f32 v4, v4, s0, v1
	v_med3_f32 v6, v6, s0, v1
	v_mov_b32_e32 v137, v5
	v_cvt_pk_fp8_f32 v137, v4, v6
	v_mul_f32_e32 v10, 0x43800000, v102
	v_mul_f32_e32 v4, 0x43800000, v90
	v_med3_f32 v6, v10, s0, v1
	v_med3_f32 v4, v4, s0, v1
	v_cvt_pk_fp8_f32 v137, v6, v4 op_sel:[0,0,1]
	v_mul_f32_e32 v4, 0x43800000, v7
	v_mul_f32_e32 v6, 0x43800000, v11
	v_med3_f32 v4, v4, s0, v1
	v_med3_f32 v6, v6, s0, v1
	v_mov_b32_e32 v138, v5
	v_cvt_pk_fp8_f32 v138, v4, v6
	v_mul_f32_e32 v7, 0x43800000, v19
	v_mul_f32_e32 v4, 0x43800000, v15
	v_med3_f32 v6, v7, s0, v1
	v_med3_f32 v4, v4, s0, v1
	v_cvt_pk_fp8_f32 v138, v6, v4 op_sel:[0,0,1]
	v_mul_f32_e32 v4, 0x43800000, v23
	v_mul_f32_e32 v6, 0x43800000, v27
	v_med3_f32 v4, v4, s0, v1
	v_med3_f32 v6, v6, s0, v1
	v_mov_b32_e32 v139, v5
	v_cvt_pk_fp8_f32 v139, v4, v6
	v_mul_f32_e32 v7, 0x43800000, v39
	v_mul_f32_e32 v4, 0x43800000, v31
	v_med3_f32 v6, v7, s0, v1
	v_med3_f32 v4, v4, s0, v1
	v_cvt_pk_fp8_f32 v139, v6, v4 op_sel:[0,0,1]
	v_mul_f32_e32 v4, 0x43800000, v43
	v_mul_f32_e32 v6, 0x43800000, v51
	v_med3_f32 v4, v4, s0, v1
	v_med3_f32 v6, v6, s0, v1
	v_mov_b32_e32 v140, v5
	v_cvt_pk_fp8_f32 v140, v4, v6
	v_mul_f32_e32 v7, 0x43800000, v71
	v_mul_f32_e32 v4, 0x43800000, v59
	v_med3_f32 v6, v7, s0, v1
	v_med3_f32 v4, v4, s0, v1
	v_cvt_pk_fp8_f32 v140, v6, v4 op_sel:[0,0,1]
	v_mul_f32_e32 v4, 0x43800000, v75
	v_mul_f32_e32 v6, 0x43800000, v83
	v_med3_f32 v4, v4, s0, v1
	v_med3_f32 v6, v6, s0, v1
	v_mov_b32_e32 v141, v5
	v_cvt_pk_fp8_f32 v141, v4, v6
	v_mul_f32_e32 v7, 0x43800000, v103
	v_mul_f32_e32 v4, 0x43800000, v91
	v_med3_f32 v6, v7, s0, v1
	v_med3_f32 v4, v4, s0, v1
	v_cvt_pk_fp8_f32 v141, v6, v4 op_sel:[0,0,1]
	v_mul_f32_e32 v4, 0x43800000, v8
	v_mul_f32_e32 v6, 0x43800000, v12
	v_med3_f32 v4, v4, s0, v1
	v_med3_f32 v6, v6, s0, v1
	v_mov_b32_e32 v142, v5
	v_cvt_pk_fp8_f32 v142, v4, v6
	v_mul_f32_e32 v7, 0x43800000, v20
	v_mul_f32_e32 v4, 0x43800000, v16
	v_med3_f32 v6, v7, s0, v1
	v_med3_f32 v4, v4, s0, v1
	v_cvt_pk_fp8_f32 v142, v6, v4 op_sel:[0,0,1]
	v_mul_f32_e32 v4, 0x43800000, v24
	v_mul_f32_e32 v6, 0x43800000, v28
	v_med3_f32 v4, v4, s0, v1
	v_med3_f32 v6, v6, s0, v1
	v_mov_b32_e32 v143, v5
	v_cvt_pk_fp8_f32 v143, v4, v6
	v_mul_f32_e32 v7, 0x43800000, v40
	v_mul_f32_e32 v4, 0x43800000, v32
	v_med3_f32 v6, v7, s0, v1
	v_med3_f32 v4, v4, s0, v1
	v_cvt_pk_fp8_f32 v143, v6, v4 op_sel:[0,0,1]
	v_mul_f32_e32 v4, 0x43800000, v44
	v_mul_f32_e32 v6, 0x43800000, v52
	v_med3_f32 v4, v4, s0, v1
	v_med3_f32 v6, v6, s0, v1
	v_mov_b32_e32 v144, v5
	v_cvt_pk_fp8_f32 v144, v4, v6
	v_mul_f32_e32 v7, 0x43800000, v72
	v_mul_f32_e32 v4, 0x43800000, v60
	v_med3_f32 v6, v7, s0, v1
	v_med3_f32 v4, v4, s0, v1
	v_cvt_pk_fp8_f32 v144, v6, v4 op_sel:[0,0,1]
	v_mul_f32_e32 v4, 0x43800000, v76
	v_mul_f32_e32 v6, 0x43800000, v84
	v_med3_f32 v4, v4, s0, v1
	v_med3_f32 v6, v6, s0, v1
	v_mov_b32_e32 v145, v5
	v_cvt_pk_fp8_f32 v145, v4, v6
	v_mul_f32_e32 v7, 0x43800000, v104
	v_mul_f32_e32 v4, 0x43800000, v92
	v_med3_f32 v6, v7, s0, v1
	v_med3_f32 v4, v4, s0, v1
	v_cvt_pk_fp8_f32 v145, v6, v4 op_sel:[0,0,1]
	v_mul_f32_e32 v4, 0x43800000, v9
	v_mul_f32_e32 v6, 0x43800000, v13
	v_med3_f32 v4, v4, s0, v1
	v_med3_f32 v8, v6, s0, v1
	v_mov_b32_e32 v6, v5
	v_cvt_pk_fp8_f32 v6, v4, v8
	v_mul_f32_e32 v7, 0x43800000, v21
	v_mul_f32_e32 v4, 0x43800000, v17
	v_med3_f32 v7, v7, s0, v1
	v_med3_f32 v4, v4, s0, v1
	v_cvt_pk_fp8_f32 v6, v7, v4 op_sel:[0,0,1]
	v_mul_f32_e32 v4, 0x43800000, v25
	v_mul_f32_e32 v7, 0x43800000, v29
	v_med3_f32 v4, v4, s0, v1
	v_med3_f32 v9, v7, s0, v1
	v_mov_b32_e32 v7, v5
	v_cvt_pk_fp8_f32 v7, v4, v9
	v_mul_f32_e32 v8, 0x43800000, v41
	v_mul_f32_e32 v4, 0x43800000, v33
	v_med3_f32 v8, v8, s0, v1
	v_med3_f32 v4, v4, s0, v1
	v_cvt_pk_fp8_f32 v7, v8, v4 op_sel:[0,0,1]
	v_mul_f32_e32 v4, 0x43800000, v45
	v_mul_f32_e32 v8, 0x43800000, v53
	v_med3_f32 v4, v4, s0, v1
	v_med3_f32 v10, v8, s0, v1
	v_mov_b32_e32 v8, v5
	v_cvt_pk_fp8_f32 v8, v4, v10
	v_mul_f32_e32 v9, 0x43800000, v73
	v_mul_f32_e32 v4, 0x43800000, v61
	v_med3_f32 v9, v9, s0, v1
	v_med3_f32 v4, v4, s0, v1
	v_cvt_pk_fp8_f32 v8, v9, v4 op_sel:[0,0,1]
	v_mul_f32_e32 v4, 0x43800000, v77
	v_mul_f32_e32 v9, 0x43800000, v85
	v_med3_f32 v4, v4, s0, v1
	v_med3_f32 v11, v9, s0, v1
	v_mov_b32_e32 v9, v5
	v_cvt_pk_fp8_f32 v9, v4, v11
	v_mul_f32_e32 v10, 0x43800000, v105
	v_mul_f32_e32 v4, 0x43800000, v93
	v_med3_f32 v10, v10, s0, v1
	v_med3_f32 v4, v4, s0, v1
	v_cvt_pk_fp8_f32 v9, v10, v4 op_sel:[0,0,1]
	ds_write_b128 v166, v[134:137] offset:34816
	ds_write_b128 v166, v[138:141] offset:35088
	ds_write_b128 v166, v[142:145] offset:35360
	ds_write_b128 v166, v[6:9] offset:35632
	s_waitcnt lgkmcnt(0)
	s_barrier
	s_mov_b32 s1, 0x600000
	v_add_co_u32_e32 v6, vcc, s1, v2
	s_mov_b32 s1, 0x602000
	s_nop 0
	v_addc_co_u32_e32 v7, vcc, 0, v3, vcc
	v_add_co_u32_e32 v10, vcc, s1, v2
	s_mov_b32 s1, 0x604000
	s_nop 0
	v_addc_co_u32_e32 v11, vcc, 0, v3, vcc
	global_load_dwordx4 v[6:9], v[6:7], off sc0 nt
	s_nop 0
	global_load_dwordx4 v[14:17], v[10:11], off sc0 nt
	v_add_co_u32_e32 v10, vcc, s1, v2
	s_mov_b32 s1, 0x606000
	s_nop 0
	v_addc_co_u32_e32 v11, vcc, 0, v3, vcc
	v_add_co_u32_e32 v12, vcc, s1, v2
	s_mov_b32 s1, 0x608000
	s_nop 0
	v_addc_co_u32_e32 v13, vcc, 0, v3, vcc
	global_load_dwordx4 v[30:33], v[10:11], off sc0 nt
	global_load_dwordx4 v[22:25], v[12:13], off sc0 nt
	v_add_co_u32_e32 v10, vcc, s1, v2
	s_mov_b32 s1, 0x60a000
	s_nop 0
	v_addc_co_u32_e32 v11, vcc, 0, v3, vcc
	v_add_co_u32_e32 v12, vcc, s1, v2
	s_mov_b32 s1, 0x60c000
	s_nop 0
	v_addc_co_u32_e32 v13, vcc, 0, v3, vcc
	global_load_dwordx4 v[38:41], v[10:11], off sc0 nt
	global_load_dwordx4 v[50:53], v[12:13], off sc0 nt
	v_add_co_u32_e32 v10, vcc, s1, v2
	s_mov_b32 s1, 0x60e000
	s_nop 0
	v_addc_co_u32_e32 v11, vcc, 0, v3, vcc
	v_add_co_u32_e32 v12, vcc, s1, v2
	s_mov_b32 s1, 0x610000
	s_nop 0
	v_addc_co_u32_e32 v13, vcc, 0, v3, vcc
	global_load_dwordx4 v[70:73], v[10:11], off sc0 nt
	global_load_dwordx4 v[58:61], v[12:13], off sc0 nt
	v_add_co_u32_e32 v10, vcc, s1, v2
	s_mov_b32 s1, 0x612000
	s_nop 0
	v_addc_co_u32_e32 v11, vcc, 0, v3, vcc
	v_add_co_u32_e32 v12, vcc, s1, v2
	s_mov_b32 s1, 0x614000
	s_nop 0
	v_addc_co_u32_e32 v13, vcc, 0, v3, vcc
	global_load_dwordx4 v[74:77], v[10:11], off sc0 nt
	global_load_dwordx4 v[82:85], v[12:13], off sc0 nt
	v_add_co_u32_e32 v10, vcc, s1, v2
	s_mov_b32 s1, 0x616000
	s_nop 0
	v_addc_co_u32_e32 v11, vcc, 0, v3, vcc
	v_add_co_u32_e32 v12, vcc, s1, v2
	s_mov_b32 s1, 0x618000
	s_nop 0
	v_addc_co_u32_e32 v13, vcc, 0, v3, vcc
	global_load_dwordx4 v[102:105], v[10:11], off sc0 nt
	global_load_dwordx4 v[90:93], v[12:13], off sc0 nt
	v_add_co_u32_e32 v10, vcc, s1, v2
	s_mov_b32 s1, 0x61a000
	s_nop 0
	v_addc_co_u32_e32 v11, vcc, 0, v3, vcc
	v_add_co_u32_e32 v12, vcc, s1, v2
	s_mov_b32 s1, 0x61c000
	s_nop 0
	v_addc_co_u32_e32 v13, vcc, 0, v3, vcc
	global_load_dwordx4 v[134:137], v[10:11], off sc0 nt
	global_load_dwordx4 v[138:141], v[12:13], off sc0 nt
	v_add_co_u32_e32 v10, vcc, s1, v2
	s_mov_b32 s1, 0x61e000
	s_nop 0
	v_addc_co_u32_e32 v11, vcc, 0, v3, vcc
	v_add_co_u32_e32 v12, vcc, s1, v2
	s_nop 1
	v_addc_co_u32_e32 v13, vcc, 0, v3, vcc
	global_load_dwordx4 v[146:149], v[10:11], off sc0 nt
	global_load_dwordx4 v[142:145], v[12:13], off sc0 nt
	ds_read_b128 v[10:13], v154 offset:34816
	ds_read_b128 v[18:21], v156 offset:34816
	ds_read_b128 v[26:29], v158 offset:34816
	ds_read_b128 v[42:45], v162 offset:34816
	s_waitcnt lgkmcnt(3)
	global_store_dwordx4 v[150:151], v[10:13], off offset:256 nt
	s_waitcnt lgkmcnt(2)
	global_store_dwordx4 v[152:153], v[18:21], off offset:256 nt
	s_waitcnt lgkmcnt(1)
	global_store_dwordx4 v[160:161], v[26:29], off offset:256 nt
	s_waitcnt lgkmcnt(0)
	global_store_dwordx4 v[164:165], v[42:45], off offset:256 nt
	s_waitcnt vmcnt(39)
	v_mul_f32_e32 v4, 0x43800000, v34
	s_waitcnt vmcnt(38)
	v_mul_f32_e32 v10, 0x43800000, v46
	v_med3_f32 v4, v4, s0, v1
	v_med3_f32 v12, v10, s0, v1
	v_mov_b32_e32 v10, v5
	v_cvt_pk_fp8_f32 v10, v4, v12
	s_waitcnt vmcnt(37)
	v_mul_f32_e32 v11, 0x43800000, v62
	s_waitcnt vmcnt(36)
	v_mul_f32_e32 v4, 0x43800000, v54
	v_med3_f32 v11, v11, s0, v1
	v_med3_f32 v4, v4, s0, v1
	v_cvt_pk_fp8_f32 v10, v11, v4 op_sel:[0,0,1]
	s_waitcnt vmcnt(35)
	v_mul_f32_e32 v4, 0x43800000, v66
	s_waitcnt vmcnt(34)
	v_mul_f32_e32 v11, 0x43800000, v78
	v_med3_f32 v4, v4, s0, v1
	v_med3_f32 v13, v11, s0, v1
	v_mov_b32_e32 v11, v5
	v_cvt_pk_fp8_f32 v11, v4, v13
	s_waitcnt vmcnt(33)
	v_mul_f32_e32 v12, 0x43800000, v94
	s_waitcnt vmcnt(32)
	v_mul_f32_e32 v4, 0x43800000, v86
	v_med3_f32 v12, v12, s0, v1
	v_med3_f32 v4, v4, s0, v1
	v_cvt_pk_fp8_f32 v11, v12, v4 op_sel:[0,0,1]
	s_waitcnt vmcnt(31)
	v_mul_f32_e32 v4, 0x43800000, v98
	s_waitcnt vmcnt(30)
	v_mul_f32_e32 v12, 0x43800000, v106
	v_med3_f32 v4, v4, s0, v1
	v_med3_f32 v18, v12, s0, v1
	v_mov_b32_e32 v12, v5
	v_cvt_pk_fp8_f32 v12, v4, v18
	s_waitcnt vmcnt(29)
	v_mul_f32_e32 v13, 0x43800000, v114
	s_waitcnt vmcnt(28)
	v_mul_f32_e32 v4, 0x43800000, v110
	v_med3_f32 v13, v13, s0, v1
	v_med3_f32 v4, v4, s0, v1
	v_cvt_pk_fp8_f32 v12, v13, v4 op_sel:[0,0,1]
	s_waitcnt vmcnt(27)
	v_mul_f32_e32 v4, 0x43800000, v118
	s_waitcnt vmcnt(26)
	v_mul_f32_e32 v13, 0x43800000, v122
	v_med3_f32 v4, v4, s0, v1
	v_med3_f32 v19, v13, s0, v1
	v_mov_b32_e32 v13, v5
	v_cvt_pk_fp8_f32 v13, v4, v19
	s_waitcnt vmcnt(25)
	v_mul_f32_e32 v18, 0x43800000, v130
	s_waitcnt vmcnt(24)
	v_mul_f32_e32 v4, 0x43800000, v126
	v_med3_f32 v18, v18, s0, v1
	v_med3_f32 v4, v4, s0, v1
	v_cvt_pk_fp8_f32 v13, v18, v4 op_sel:[0,0,1]
	v_mul_f32_e32 v4, 0x43800000, v35
	v_mul_f32_e32 v18, 0x43800000, v47
	v_med3_f32 v4, v4, s0, v1
	v_med3_f32 v20, v18, s0, v1
	v_mov_b32_e32 v18, v5
	v_cvt_pk_fp8_f32 v18, v4, v20
	v_mul_f32_e32 v19, 0x43800000, v63
	v_mul_f32_e32 v4, 0x43800000, v55
	v_med3_f32 v19, v19, s0, v1
	v_med3_f32 v4, v4, s0, v1
	v_cvt_pk_fp8_f32 v18, v19, v4 op_sel:[0,0,1]
	v_mul_f32_e32 v4, 0x43800000, v67
	v_mul_f32_e32 v19, 0x43800000, v79
	v_med3_f32 v4, v4, s0, v1
	v_med3_f32 v21, v19, s0, v1
	v_mov_b32_e32 v19, v5
	v_cvt_pk_fp8_f32 v19, v4, v21
	v_mul_f32_e32 v20, 0x43800000, v95
	v_mul_f32_e32 v4, 0x43800000, v87
	v_med3_f32 v20, v20, s0, v1
	v_med3_f32 v4, v4, s0, v1
	v_cvt_pk_fp8_f32 v19, v20, v4 op_sel:[0,0,1]
	v_mul_f32_e32 v4, 0x43800000, v99
	v_mul_f32_e32 v20, 0x43800000, v107
	v_med3_f32 v4, v4, s0, v1
	v_med3_f32 v26, v20, s0, v1
	v_mov_b32_e32 v20, v5
	v_cvt_pk_fp8_f32 v20, v4, v26
	v_mul_f32_e32 v21, 0x43800000, v115
	v_mul_f32_e32 v4, 0x43800000, v111
	v_med3_f32 v21, v21, s0, v1
	v_med3_f32 v4, v4, s0, v1
	v_cvt_pk_fp8_f32 v20, v21, v4 op_sel:[0,0,1]
	v_mul_f32_e32 v4, 0x43800000, v119
	v_mul_f32_e32 v21, 0x43800000, v123
	v_med3_f32 v4, v4, s0, v1
	v_med3_f32 v27, v21, s0, v1
	v_mov_b32_e32 v21, v5
	v_cvt_pk_fp8_f32 v21, v4, v27
	v_mul_f32_e32 v26, 0x43800000, v131
	v_mul_f32_e32 v4, 0x43800000, v127
	v_med3_f32 v26, v26, s0, v1
	v_med3_f32 v4, v4, s0, v1
	v_cvt_pk_fp8_f32 v21, v26, v4 op_sel:[0,0,1]
	v_mul_f32_e32 v4, 0x43800000, v36
	v_mul_f32_e32 v26, 0x43800000, v48
	v_med3_f32 v4, v4, s0, v1
	v_med3_f32 v28, v26, s0, v1
	v_mov_b32_e32 v26, v5
	v_cvt_pk_fp8_f32 v26, v4, v28
	v_mul_f32_e32 v27, 0x43800000, v64
	v_mul_f32_e32 v4, 0x43800000, v56
	v_med3_f32 v27, v27, s0, v1
	v_med3_f32 v4, v4, s0, v1
	v_cvt_pk_fp8_f32 v26, v27, v4 op_sel:[0,0,1]
	v_mul_f32_e32 v4, 0x43800000, v68
	v_mul_f32_e32 v27, 0x43800000, v80
	v_med3_f32 v4, v4, s0, v1
	v_med3_f32 v29, v27, s0, v1
	v_mov_b32_e32 v27, v5
	v_cvt_pk_fp8_f32 v27, v4, v29
	v_mul_f32_e32 v28, 0x43800000, v96
	v_mul_f32_e32 v4, 0x43800000, v88
	v_med3_f32 v28, v28, s0, v1
	v_med3_f32 v4, v4, s0, v1
	v_cvt_pk_fp8_f32 v27, v28, v4 op_sel:[0,0,1]
	v_mul_f32_e32 v4, 0x43800000, v100
	v_mul_f32_e32 v28, 0x43800000, v108
	v_med3_f32 v4, v4, s0, v1
	v_med3_f32 v34, v28, s0, v1
	v_mov_b32_e32 v28, v5
	v_cvt_pk_fp8_f32 v28, v4, v34
	v_mul_f32_e32 v29, 0x43800000, v116
	v_mul_f32_e32 v4, 0x43800000, v112
	v_med3_f32 v29, v29, s0, v1
	v_med3_f32 v4, v4, s0, v1
	v_cvt_pk_fp8_f32 v28, v29, v4 op_sel:[0,0,1]
	v_mul_f32_e32 v4, 0x43800000, v120
	v_mul_f32_e32 v29, 0x43800000, v124
	v_med3_f32 v4, v4, s0, v1
	v_med3_f32 v35, v29, s0, v1
	v_mov_b32_e32 v29, v5
	v_cvt_pk_fp8_f32 v29, v4, v35
	v_mul_f32_e32 v34, 0x43800000, v132
	v_mul_f32_e32 v4, 0x43800000, v128
	v_med3_f32 v34, v34, s0, v1
	v_med3_f32 v4, v4, s0, v1
	v_cvt_pk_fp8_f32 v29, v34, v4 op_sel:[0,0,1]
	v_mul_f32_e32 v4, 0x43800000, v37
	v_mul_f32_e32 v34, 0x43800000, v49
	v_med3_f32 v4, v4, s0, v1
	v_med3_f32 v36, v34, s0, v1
	v_mov_b32_e32 v34, v5
	v_cvt_pk_fp8_f32 v34, v4, v36
	v_mul_f32_e32 v35, 0x43800000, v65
	v_mul_f32_e32 v4, 0x43800000, v57
	v_med3_f32 v35, v35, s0, v1
	v_med3_f32 v4, v4, s0, v1
	v_cvt_pk_fp8_f32 v34, v35, v4 op_sel:[0,0,1]
	v_mul_f32_e32 v4, 0x43800000, v69
	v_mul_f32_e32 v35, 0x43800000, v81
	v_med3_f32 v4, v4, s0, v1
	v_med3_f32 v37, v35, s0, v1
	v_mov_b32_e32 v35, v5
	v_cvt_pk_fp8_f32 v35, v4, v37
	v_mul_f32_e32 v36, 0x43800000, v97
	v_mul_f32_e32 v4, 0x43800000, v89
	v_med3_f32 v36, v36, s0, v1
	v_med3_f32 v4, v4, s0, v1
	v_cvt_pk_fp8_f32 v35, v36, v4 op_sel:[0,0,1]
	v_mul_f32_e32 v4, 0x43800000, v101
	v_mul_f32_e32 v36, 0x43800000, v109
	v_med3_f32 v4, v4, s0, v1
	v_med3_f32 v42, v36, s0, v1
	v_mov_b32_e32 v36, v5
	v_cvt_pk_fp8_f32 v36, v4, v42
	v_mul_f32_e32 v37, 0x43800000, v117
	v_mul_f32_e32 v4, 0x43800000, v113
	v_med3_f32 v37, v37, s0, v1
	v_med3_f32 v4, v4, s0, v1
	v_cvt_pk_fp8_f32 v36, v37, v4 op_sel:[0,0,1]
	v_mul_f32_e32 v4, 0x43800000, v121
	v_mul_f32_e32 v37, 0x43800000, v125
	v_med3_f32 v4, v4, s0, v1
	v_med3_f32 v43, v37, s0, v1
	v_mov_b32_e32 v37, v5
	v_cvt_pk_fp8_f32 v37, v4, v43
	v_mul_f32_e32 v42, 0x43800000, v133
	v_mul_f32_e32 v4, 0x43800000, v129
	v_med3_f32 v42, v42, s0, v1
	v_med3_f32 v4, v4, s0, v1
	v_cvt_pk_fp8_f32 v37, v42, v4 op_sel:[0,0,1]
	ds_write_b128 v166, v[10:13]
	ds_write_b128 v166, v[18:21] offset:272
	ds_write_b128 v166, v[26:29] offset:544
	ds_write_b128 v166, v[34:37] offset:816
	s_waitcnt lgkmcnt(0)
	s_barrier
	s_mov_b32 s1, 0x800000
	v_add_co_u32_e32 v10, vcc, s1, v2
	s_mov_b32 s1, 0x802000
	s_nop 0
	v_addc_co_u32_e32 v11, vcc, 0, v3, vcc
	v_add_co_u32_e32 v18, vcc, s1, v2
	s_mov_b32 s1, 0x804000
	s_nop 0
	v_addc_co_u32_e32 v19, vcc, 0, v3, vcc
	v_add_co_u32_e32 v26, vcc, s1, v2
	s_mov_b32 s1, 0x806000
	s_nop 0
	v_addc_co_u32_e32 v27, vcc, 0, v3, vcc
	v_add_co_u32_e32 v28, vcc, s1, v2
	s_mov_b32 s1, 0x808000
	s_nop 0
	v_addc_co_u32_e32 v29, vcc, 0, v3, vcc
	v_add_co_u32_e32 v42, vcc, s1, v2
	s_mov_b32 s1, 0x80a000
	s_nop 0
	v_addc_co_u32_e32 v43, vcc, 0, v3, vcc
	v_add_co_u32_e32 v46, vcc, s1, v2
	s_mov_b32 s1, 0x80c000
	s_nop 0
	v_addc_co_u32_e32 v47, vcc, 0, v3, vcc
	v_add_co_u32_e32 v54, vcc, s1, v2
	s_mov_b32 s1, 0x80e000
	s_nop 0
	v_addc_co_u32_e32 v55, vcc, 0, v3, vcc
	v_add_co_u32_e32 v56, vcc, s1, v2
	s_mov_b32 s1, 0x810000
	s_nop 0
	v_addc_co_u32_e32 v57, vcc, 0, v3, vcc
	v_add_co_u32_e32 v66, vcc, s1, v2
	s_mov_b32 s1, 0x812000
	s_nop 0
	v_addc_co_u32_e32 v67, vcc, 0, v3, vcc
	v_add_co_u32_e32 v78, vcc, s1, v2
	s_mov_b32 s1, 0x814000
	s_nop 0
	v_addc_co_u32_e32 v79, vcc, 0, v3, vcc
	v_add_co_u32_e32 v86, vcc, s1, v2
	s_mov_b32 s1, 0x816000
	s_nop 0
	v_addc_co_u32_e32 v87, vcc, 0, v3, vcc
	v_add_co_u32_e32 v88, vcc, s1, v2
	s_mov_b32 s1, 0x818000
	s_nop 0
	v_addc_co_u32_e32 v89, vcc, 0, v3, vcc
	v_add_co_u32_e32 v98, vcc, s1, v2
	s_mov_b32 s1, 0x81a000
	s_nop 0
	v_addc_co_u32_e32 v99, vcc, 0, v3, vcc
	v_add_co_u32_e32 v106, vcc, s1, v2
	s_mov_b32 s1, 0x81c000
	s_nop 0
	v_addc_co_u32_e32 v107, vcc, 0, v3, vcc
	global_load_dwordx4 v[10:13], v[10:11], off sc0 nt
	s_nop 0
	global_load_dwordx4 v[18:21], v[18:19], off sc0 nt
	s_nop 0
	global_load_dwordx4 v[34:37], v[26:27], off sc0 nt
	s_nop 0
	global_load_dwordx4 v[26:29], v[28:29], off sc0 nt
	s_nop 0
	global_load_dwordx4 v[42:45], v[42:43], off sc0 nt
	s_nop 0
	global_load_dwordx4 v[46:49], v[46:47], off sc0 nt
	s_nop 0
	global_load_dwordx4 v[62:65], v[54:55], off sc0 nt
	s_nop 0
	global_load_dwordx4 v[54:57], v[56:57], off sc0 nt
	s_nop 0
	global_load_dwordx4 v[66:69], v[66:67], off sc0 nt
	s_nop 0
	global_load_dwordx4 v[78:81], v[78:79], off sc0 nt
	s_nop 0
	global_load_dwordx4 v[94:97], v[86:87], off sc0 nt
	s_nop 0
	global_load_dwordx4 v[86:89], v[88:89], off sc0 nt
	s_nop 0
	global_load_dwordx4 v[98:101], v[98:99], off sc0 nt
	s_nop 0
	global_load_dwordx4 v[110:113], v[106:107], off sc0 nt
	v_add_co_u32_e32 v106, vcc, s1, v2
	s_mov_b32 s1, 0x81e000
	s_nop 0
	v_addc_co_u32_e32 v107, vcc, 0, v3, vcc
	v_add_co_u32_e32 v108, vcc, s1, v2
	s_nop 1
	v_addc_co_u32_e32 v109, vcc, 0, v3, vcc
	global_load_dwordx4 v[126:129], v[106:107], off sc0 nt
	global_load_dwordx4 v[118:121], v[108:109], off sc0 nt
	ds_read_b128 v[106:109], v154
	ds_read_b128 v[114:117], v156
	ds_read_b128 v[122:125], v158
	ds_read_b128 v[130:133], v162
	s_waitcnt lgkmcnt(3)
	global_store_dwordx4 v[150:151], v[106:109], off offset:512 nt
	s_waitcnt lgkmcnt(2)
	global_store_dwordx4 v[152:153], v[114:117], off offset:512 nt
	s_waitcnt lgkmcnt(1)
	global_store_dwordx4 v[160:161], v[122:125], off offset:512 nt
	s_waitcnt lgkmcnt(0)
	global_store_dwordx4 v[164:165], v[130:133], off offset:512 nt
	s_waitcnt vmcnt(39)
	v_mul_f32_e32 v4, 0x43800000, v6
	s_waitcnt vmcnt(38)
	v_mul_f32_e32 v6, 0x43800000, v14
	v_med3_f32 v4, v4, s0, v1
	v_med3_f32 v6, v6, s0, v1
	v_mov_b32_e32 v106, v5
	v_cvt_pk_fp8_f32 v106, v4, v6
	s_waitcnt vmcnt(37)
	v_mul_f32_e32 v14, 0x43800000, v30
	s_waitcnt vmcnt(36)
	v_mul_f32_e32 v4, 0x43800000, v22
	v_med3_f32 v6, v14, s0, v1
	v_med3_f32 v4, v4, s0, v1
	v_cvt_pk_fp8_f32 v106, v6, v4 op_sel:[0,0,1]
	s_waitcnt vmcnt(35)
	v_mul_f32_e32 v4, 0x43800000, v38
	s_waitcnt vmcnt(34)
	v_mul_f32_e32 v6, 0x43800000, v50
	v_med3_f32 v4, v4, s0, v1
	v_med3_f32 v6, v6, s0, v1
	v_mov_b32_e32 v107, v5
	v_cvt_pk_fp8_f32 v107, v4, v6
	s_waitcnt vmcnt(33)
	v_mul_f32_e32 v14, 0x43800000, v70
	s_waitcnt vmcnt(32)
	v_mul_f32_e32 v4, 0x43800000, v58
	v_med3_f32 v6, v14, s0, v1
	v_med3_f32 v4, v4, s0, v1
	v_cvt_pk_fp8_f32 v107, v6, v4 op_sel:[0,0,1]
	s_waitcnt vmcnt(31)
	v_mul_f32_e32 v4, 0x43800000, v74
	s_waitcnt vmcnt(30)
	v_mul_f32_e32 v6, 0x43800000, v82
	v_med3_f32 v4, v4, s0, v1
	v_med3_f32 v6, v6, s0, v1
	v_mov_b32_e32 v108, v5
	v_cvt_pk_fp8_f32 v108, v4, v6
	s_waitcnt vmcnt(29)
	v_mul_f32_e32 v14, 0x43800000, v102
	s_waitcnt vmcnt(28)
	v_mul_f32_e32 v4, 0x43800000, v90
	v_med3_f32 v6, v14, s0, v1
	v_med3_f32 v4, v4, s0, v1
	v_cvt_pk_fp8_f32 v108, v6, v4 op_sel:[0,0,1]
	s_waitcnt vmcnt(27)
	v_mul_f32_e32 v4, 0x43800000, v134
	s_waitcnt vmcnt(26)
	v_mul_f32_e32 v6, 0x43800000, v138
	v_med3_f32 v4, v4, s0, v1
	v_med3_f32 v6, v6, s0, v1
	v_mov_b32_e32 v109, v5
	v_cvt_pk_fp8_f32 v109, v4, v6
	s_waitcnt vmcnt(25)
	v_mul_f32_e32 v14, 0x43800000, v146
	s_waitcnt vmcnt(24)
	v_mul_f32_e32 v4, 0x43800000, v142
	v_med3_f32 v6, v14, s0, v1
	v_med3_f32 v4, v4, s0, v1
	v_cvt_pk_fp8_f32 v109, v6, v4 op_sel:[0,0,1]
	v_mul_f32_e32 v4, 0x43800000, v7
	v_mul_f32_e32 v6, 0x43800000, v15
	v_med3_f32 v4, v4, s0, v1
	v_med3_f32 v6, v6, s0, v1
	v_mov_b32_e32 v114, v5
	v_cvt_pk_fp8_f32 v114, v4, v6
	v_mul_f32_e32 v7, 0x43800000, v31
	v_mul_f32_e32 v4, 0x43800000, v23
	v_med3_f32 v6, v7, s0, v1
	v_med3_f32 v4, v4, s0, v1
	v_cvt_pk_fp8_f32 v114, v6, v4 op_sel:[0,0,1]
	v_mul_f32_e32 v4, 0x43800000, v39
	v_mul_f32_e32 v6, 0x43800000, v51
	v_med3_f32 v4, v4, s0, v1
	v_med3_f32 v6, v6, s0, v1
	v_mov_b32_e32 v115, v5
	v_cvt_pk_fp8_f32 v115, v4, v6
	v_mul_f32_e32 v7, 0x43800000, v71
	v_mul_f32_e32 v4, 0x43800000, v59
	v_med3_f32 v6, v7, s0, v1
	v_med3_f32 v4, v4, s0, v1
	v_cvt_pk_fp8_f32 v115, v6, v4 op_sel:[0,0,1]
	v_mul_f32_e32 v4, 0x43800000, v75
	v_mul_f32_e32 v6, 0x43800000, v83
	v_med3_f32 v4, v4, s0, v1
	v_med3_f32 v6, v6, s0, v1
	v_mov_b32_e32 v116, v5
	v_cvt_pk_fp8_f32 v116, v4, v6
	v_mul_f32_e32 v7, 0x43800000, v103
	v_mul_f32_e32 v4, 0x43800000, v91
	v_med3_f32 v6, v7, s0, v1
	v_med3_f32 v4, v4, s0, v1
	v_cvt_pk_fp8_f32 v116, v6, v4 op_sel:[0,0,1]
	v_mul_f32_e32 v4, 0x43800000, v135
	v_mul_f32_e32 v6, 0x43800000, v139
	v_med3_f32 v4, v4, s0, v1
	v_med3_f32 v6, v6, s0, v1
	v_mov_b32_e32 v117, v5
	v_cvt_pk_fp8_f32 v117, v4, v6
	v_mul_f32_e32 v7, 0x43800000, v147
	v_mul_f32_e32 v4, 0x43800000, v143
	v_med3_f32 v6, v7, s0, v1
	v_med3_f32 v4, v4, s0, v1
	v_cvt_pk_fp8_f32 v117, v6, v4 op_sel:[0,0,1]
	v_mul_f32_e32 v4, 0x43800000, v8
	v_mul_f32_e32 v6, 0x43800000, v16
	v_med3_f32 v4, v4, s0, v1
	v_med3_f32 v6, v6, s0, v1
	v_mov_b32_e32 v122, v5
	v_cvt_pk_fp8_f32 v122, v4, v6
	v_mul_f32_e32 v7, 0x43800000, v32
	v_mul_f32_e32 v4, 0x43800000, v24
	v_med3_f32 v6, v7, s0, v1
	v_med3_f32 v4, v4, s0, v1
	v_cvt_pk_fp8_f32 v122, v6, v4 op_sel:[0,0,1]
	v_mul_f32_e32 v4, 0x43800000, v40
	v_mul_f32_e32 v6, 0x43800000, v52
	v_med3_f32 v4, v4, s0, v1
	v_med3_f32 v6, v6, s0, v1
	v_mov_b32_e32 v123, v5
	v_cvt_pk_fp8_f32 v123, v4, v6
	v_mul_f32_e32 v7, 0x43800000, v72
	v_mul_f32_e32 v4, 0x43800000, v60
	v_med3_f32 v6, v7, s0, v1
	v_med3_f32 v4, v4, s0, v1
	v_cvt_pk_fp8_f32 v123, v6, v4 op_sel:[0,0,1]
	v_mul_f32_e32 v4, 0x43800000, v76
	v_mul_f32_e32 v6, 0x43800000, v84
	v_med3_f32 v4, v4, s0, v1
	v_med3_f32 v6, v6, s0, v1
	v_mov_b32_e32 v124, v5
	v_cvt_pk_fp8_f32 v124, v4, v6
	v_mul_f32_e32 v7, 0x43800000, v104
	v_mul_f32_e32 v4, 0x43800000, v92
	v_med3_f32 v6, v7, s0, v1
	v_med3_f32 v4, v4, s0, v1
	v_cvt_pk_fp8_f32 v124, v6, v4 op_sel:[0,0,1]
	v_mul_f32_e32 v4, 0x43800000, v136
	v_mul_f32_e32 v6, 0x43800000, v140
	v_med3_f32 v4, v4, s0, v1
	v_med3_f32 v6, v6, s0, v1
	v_mov_b32_e32 v125, v5
	v_cvt_pk_fp8_f32 v125, v4, v6
	v_mul_f32_e32 v7, 0x43800000, v148
	v_mul_f32_e32 v4, 0x43800000, v144
	v_med3_f32 v6, v7, s0, v1
	v_med3_f32 v4, v4, s0, v1
	v_cvt_pk_fp8_f32 v125, v6, v4 op_sel:[0,0,1]
	v_mul_f32_e32 v4, 0x43800000, v9
	v_mul_f32_e32 v6, 0x43800000, v17
	v_med3_f32 v4, v4, s0, v1
	v_med3_f32 v8, v6, s0, v1
	v_mov_b32_e32 v6, v5
	v_cvt_pk_fp8_f32 v6, v4, v8
	v_mul_f32_e32 v7, 0x43800000, v33
	v_mul_f32_e32 v4, 0x43800000, v25
	v_med3_f32 v7, v7, s0, v1
	v_med3_f32 v4, v4, s0, v1
	v_cvt_pk_fp8_f32 v6, v7, v4 op_sel:[0,0,1]
	v_mul_f32_e32 v4, 0x43800000, v41
	v_mul_f32_e32 v7, 0x43800000, v53
	v_med3_f32 v4, v4, s0, v1
	v_med3_f32 v9, v7, s0, v1
	v_mov_b32_e32 v7, v5
	v_cvt_pk_fp8_f32 v7, v4, v9
	v_mul_f32_e32 v8, 0x43800000, v73
	v_mul_f32_e32 v4, 0x43800000, v61
	v_med3_f32 v8, v8, s0, v1
	v_med3_f32 v4, v4, s0, v1
	v_cvt_pk_fp8_f32 v7, v8, v4 op_sel:[0,0,1]
	v_mul_f32_e32 v4, 0x43800000, v77
	v_mul_f32_e32 v8, 0x43800000, v85
	v_med3_f32 v4, v4, s0, v1
	v_med3_f32 v14, v8, s0, v1
	v_mov_b32_e32 v8, v5
	v_cvt_pk_fp8_f32 v8, v4, v14
	v_mul_f32_e32 v9, 0x43800000, v105
	v_mul_f32_e32 v4, 0x43800000, v93
	v_med3_f32 v9, v9, s0, v1
	v_med3_f32 v4, v4, s0, v1
	v_cvt_pk_fp8_f32 v8, v9, v4 op_sel:[0,0,1]
	v_mul_f32_e32 v4, 0x43800000, v137
	v_mul_f32_e32 v9, 0x43800000, v141
	v_med3_f32 v4, v4, s0, v1
	v_med3_f32 v15, v9, s0, v1
	v_mov_b32_e32 v9, v5
	v_cvt_pk_fp8_f32 v9, v4, v15
	v_mul_f32_e32 v14, 0x43800000, v149
	v_mul_f32_e32 v4, 0x43800000, v145
	v_med3_f32 v14, v14, s0, v1
	v_med3_f32 v4, v4, s0, v1
	v_cvt_pk_fp8_f32 v9, v14, v4 op_sel:[0,0,1]
	ds_write_b128 v166, v[106:109] offset:34816
	ds_write_b128 v166, v[114:117] offset:35088
	ds_write_b128 v166, v[122:125] offset:35360
	ds_write_b128 v166, v[6:9] offset:35632
	s_waitcnt lgkmcnt(0)
	s_barrier
	s_mov_b32 s1, 0xa00000
	v_add_co_u32_e32 v6, vcc, s1, v2
	s_mov_b32 s1, 0xa02000
	s_nop 0
	v_addc_co_u32_e32 v7, vcc, 0, v3, vcc
	v_add_co_u32_e32 v14, vcc, s1, v2
	s_mov_b32 s1, 0xa04000
	s_nop 0
	v_addc_co_u32_e32 v15, vcc, 0, v3, vcc
	v_add_co_u32_e32 v22, vcc, s1, v2
	s_mov_b32 s1, 0xa06000
	s_nop 0
	v_addc_co_u32_e32 v23, vcc, 0, v3, vcc
	v_add_co_u32_e32 v24, vcc, s1, v2
	s_mov_b32 s1, 0xa08000
	s_nop 0
	v_addc_co_u32_e32 v25, vcc, 0, v3, vcc
	v_add_co_u32_e32 v38, vcc, s1, v2
	s_mov_b32 s1, 0xa0a000
	s_nop 0
	v_addc_co_u32_e32 v39, vcc, 0, v3, vcc
	v_add_co_u32_e32 v50, vcc, s1, v2
	s_mov_b32 s1, 0xa0c000
	s_nop 0
	v_addc_co_u32_e32 v51, vcc, 0, v3, vcc
	v_add_co_u32_e32 v58, vcc, s1, v2
	s_mov_b32 s1, 0xa0e000
	s_nop 0
	v_addc_co_u32_e32 v59, vcc, 0, v3, vcc
	v_add_co_u32_e32 v60, vcc, s1, v2
	s_mov_b32 s1, 0xa10000
	s_nop 0
	v_addc_co_u32_e32 v61, vcc, 0, v3, vcc
	v_add_co_u32_e32 v74, vcc, s1, v2
	s_mov_b32 s1, 0xa12000
	s_nop 0
	v_addc_co_u32_e32 v75, vcc, 0, v3, vcc
	v_add_co_u32_e32 v82, vcc, s1, v2
	s_mov_b32 s1, 0xa14000
	s_nop 0
	v_addc_co_u32_e32 v83, vcc, 0, v3, vcc
	v_add_co_u32_e32 v90, vcc, s1, v2
	s_mov_b32 s1, 0xa16000
	s_nop 0
	v_addc_co_u32_e32 v91, vcc, 0, v3, vcc
	v_add_co_u32_e32 v92, vcc, s1, v2
	s_mov_b32 s1, 0xa18000
	s_nop 0
	v_addc_co_u32_e32 v93, vcc, 0, v3, vcc
	v_add_co_u32_e32 v106, vcc, s1, v2
	s_mov_b32 s1, 0xa1a000
	s_nop 0
	v_addc_co_u32_e32 v107, vcc, 0, v3, vcc
	v_add_co_u32_e32 v114, vcc, s1, v2
	s_mov_b32 s1, 0xa1c000
	s_nop 0
	v_addc_co_u32_e32 v115, vcc, 0, v3, vcc
	v_add_co_u32_e32 v122, vcc, s1, v2
	s_mov_b32 s1, 0xa1e000
	s_nop 0
	v_addc_co_u32_e32 v123, vcc, 0, v3, vcc
	v_add_co_u32_e32 v124, vcc, s1, v2
	global_load_dwordx4 v[6:9], v[6:7], off sc0 nt
	s_nop 0
	global_load_dwordx4 v[14:17], v[14:15], off sc0 nt
	v_addc_co_u32_e32 v125, vcc, 0, v3, vcc
	global_load_dwordx4 v[30:33], v[22:23], off sc0 nt
	s_nop 0
	global_load_dwordx4 v[22:25], v[24:25], off sc0 nt
	s_nop 0
	global_load_dwordx4 v[38:41], v[38:39], off sc0 nt
	s_nop 0
	global_load_dwordx4 v[50:53], v[50:51], off sc0 nt
	s_nop 0
	global_load_dwordx4 v[70:73], v[58:59], off sc0 nt
	s_nop 0
	global_load_dwordx4 v[58:61], v[60:61], off sc0 nt
	s_nop 0
	global_load_dwordx4 v[74:77], v[74:75], off sc0 nt
	s_nop 0
	global_load_dwordx4 v[82:85], v[82:83], off sc0 nt
	s_nop 0
	global_load_dwordx4 v[102:105], v[90:91], off sc0 nt
	s_nop 0
	global_load_dwordx4 v[90:93], v[92:93], off sc0 nt
	s_nop 0
	global_load_dwordx4 v[106:109], v[106:107], off sc0 nt
	s_nop 0
	global_load_dwordx4 v[114:117], v[114:115], off sc0 nt
	s_nop 0
	global_load_dwordx4 v[130:133], v[122:123], off sc0 nt
	s_nop 0
	global_load_dwordx4 v[122:125], v[124:125], off sc0 nt
	ds_read_b128 v[134:137], v154 offset:34816
	ds_read_b128 v[138:141], v156 offset:34816
	ds_read_b128 v[142:145], v158 offset:34816
	ds_read_b128 v[146:149], v162 offset:34816
	s_waitcnt lgkmcnt(3)
	global_store_dwordx4 v[150:151], v[134:137], off offset:768 nt
	s_waitcnt lgkmcnt(2)
	global_store_dwordx4 v[152:153], v[138:141], off offset:768 nt
	s_waitcnt lgkmcnt(1)
	global_store_dwordx4 v[160:161], v[142:145], off offset:768 nt
	s_waitcnt lgkmcnt(0)
	global_store_dwordx4 v[164:165], v[146:149], off offset:768 nt
	s_waitcnt vmcnt(39)
	v_mul_f32_e32 v4, 0x43800000, v10
	s_waitcnt vmcnt(38)
	v_mul_f32_e32 v10, 0x43800000, v18
	v_med3_f32 v4, v4, s0, v1
	v_med3_f32 v10, v10, s0, v1
	v_mov_b32_e32 v134, v5
	v_cvt_pk_fp8_f32 v134, v4, v10
	s_waitcnt vmcnt(37)
	v_mul_f32_e32 v18, 0x43800000, v34
	s_waitcnt vmcnt(36)
	v_mul_f32_e32 v4, 0x43800000, v26
	v_med3_f32 v10, v18, s0, v1
	v_med3_f32 v4, v4, s0, v1
	v_cvt_pk_fp8_f32 v134, v10, v4 op_sel:[0,0,1]
	s_waitcnt vmcnt(35)
	v_mul_f32_e32 v4, 0x43800000, v42
	s_waitcnt vmcnt(34)
	v_mul_f32_e32 v10, 0x43800000, v46
	v_med3_f32 v4, v4, s0, v1
	v_med3_f32 v10, v10, s0, v1
	v_mov_b32_e32 v135, v5
	v_cvt_pk_fp8_f32 v135, v4, v10
	s_waitcnt vmcnt(33)
	v_mul_f32_e32 v18, 0x43800000, v62
	s_waitcnt vmcnt(32)
	v_mul_f32_e32 v4, 0x43800000, v54
	v_med3_f32 v10, v18, s0, v1
	v_med3_f32 v4, v4, s0, v1
	v_cvt_pk_fp8_f32 v135, v10, v4 op_sel:[0,0,1]
	s_waitcnt vmcnt(31)
	v_mul_f32_e32 v4, 0x43800000, v66
	s_waitcnt vmcnt(30)
	v_mul_f32_e32 v10, 0x43800000, v78
	v_med3_f32 v4, v4, s0, v1
	v_med3_f32 v10, v10, s0, v1
	v_mov_b32_e32 v136, v5
	v_cvt_pk_fp8_f32 v136, v4, v10
	s_waitcnt vmcnt(29)
	v_mul_f32_e32 v18, 0x43800000, v94
	s_waitcnt vmcnt(28)
	v_mul_f32_e32 v4, 0x43800000, v86
	v_med3_f32 v10, v18, s0, v1
	v_med3_f32 v4, v4, s0, v1
	v_cvt_pk_fp8_f32 v136, v10, v4 op_sel:[0,0,1]
	s_waitcnt vmcnt(27)
	v_mul_f32_e32 v4, 0x43800000, v98
	s_waitcnt vmcnt(26)
	v_mul_f32_e32 v10, 0x43800000, v110
	v_med3_f32 v4, v4, s0, v1
	v_med3_f32 v10, v10, s0, v1
	v_mov_b32_e32 v137, v5
	v_cvt_pk_fp8_f32 v137, v4, v10
	s_waitcnt vmcnt(25)
	v_mul_f32_e32 v18, 0x43800000, v126
	s_waitcnt vmcnt(24)
	v_mul_f32_e32 v4, 0x43800000, v118
	v_med3_f32 v10, v18, s0, v1
	v_med3_f32 v4, v4, s0, v1
	v_cvt_pk_fp8_f32 v137, v10, v4 op_sel:[0,0,1]
	v_mul_f32_e32 v4, 0x43800000, v11
	v_mul_f32_e32 v10, 0x43800000, v19
	v_med3_f32 v4, v4, s0, v1
	v_med3_f32 v10, v10, s0, v1
	v_mov_b32_e32 v138, v5
	v_cvt_pk_fp8_f32 v138, v4, v10
	v_mul_f32_e32 v11, 0x43800000, v35
	v_mul_f32_e32 v4, 0x43800000, v27
	v_med3_f32 v10, v11, s0, v1
	v_med3_f32 v4, v4, s0, v1
	v_cvt_pk_fp8_f32 v138, v10, v4 op_sel:[0,0,1]
	v_mul_f32_e32 v4, 0x43800000, v43
	v_mul_f32_e32 v10, 0x43800000, v47
	v_med3_f32 v4, v4, s0, v1
	v_med3_f32 v10, v10, s0, v1
	v_mov_b32_e32 v139, v5
	v_cvt_pk_fp8_f32 v139, v4, v10
	v_mul_f32_e32 v11, 0x43800000, v63
	v_mul_f32_e32 v4, 0x43800000, v55
	v_med3_f32 v10, v11, s0, v1
	v_med3_f32 v4, v4, s0, v1
	v_cvt_pk_fp8_f32 v139, v10, v4 op_sel:[0,0,1]
	v_mul_f32_e32 v4, 0x43800000, v67
	v_mul_f32_e32 v10, 0x43800000, v79
	v_med3_f32 v4, v4, s0, v1
	v_med3_f32 v10, v10, s0, v1
	v_mov_b32_e32 v140, v5
	v_cvt_pk_fp8_f32 v140, v4, v10
	v_mul_f32_e32 v11, 0x43800000, v95
	v_mul_f32_e32 v4, 0x43800000, v87
	v_med3_f32 v10, v11, s0, v1
	v_med3_f32 v4, v4, s0, v1
	v_cvt_pk_fp8_f32 v140, v10, v4 op_sel:[0,0,1]
	v_mul_f32_e32 v4, 0x43800000, v99
	v_mul_f32_e32 v10, 0x43800000, v111
	v_med3_f32 v4, v4, s0, v1
	v_med3_f32 v10, v10, s0, v1
	v_mov_b32_e32 v141, v5
	v_cvt_pk_fp8_f32 v141, v4, v10
	v_mul_f32_e32 v11, 0x43800000, v127
	v_mul_f32_e32 v4, 0x43800000, v119
	v_med3_f32 v10, v11, s0, v1
	v_med3_f32 v4, v4, s0, v1
	v_cvt_pk_fp8_f32 v141, v10, v4 op_sel:[0,0,1]
	v_mul_f32_e32 v4, 0x43800000, v12
	v_mul_f32_e32 v10, 0x43800000, v20
	v_med3_f32 v4, v4, s0, v1
	v_med3_f32 v10, v10, s0, v1
	v_mov_b32_e32 v142, v5
	v_cvt_pk_fp8_f32 v142, v4, v10
	v_mul_f32_e32 v11, 0x43800000, v36
	v_mul_f32_e32 v4, 0x43800000, v28
	v_med3_f32 v10, v11, s0, v1
	v_med3_f32 v4, v4, s0, v1
	v_cvt_pk_fp8_f32 v142, v10, v4 op_sel:[0,0,1]
	v_mul_f32_e32 v4, 0x43800000, v44
	v_mul_f32_e32 v10, 0x43800000, v48
	v_med3_f32 v4, v4, s0, v1
	v_med3_f32 v10, v10, s0, v1
	v_mov_b32_e32 v143, v5
	v_cvt_pk_fp8_f32 v143, v4, v10
	v_mul_f32_e32 v11, 0x43800000, v64
	v_mul_f32_e32 v4, 0x43800000, v56
	v_med3_f32 v10, v11, s0, v1
	v_med3_f32 v4, v4, s0, v1
	v_cvt_pk_fp8_f32 v143, v10, v4 op_sel:[0,0,1]
	v_mul_f32_e32 v4, 0x43800000, v68
	v_mul_f32_e32 v10, 0x43800000, v80
	v_med3_f32 v4, v4, s0, v1
	v_med3_f32 v10, v10, s0, v1
	v_mov_b32_e32 v144, v5
	v_cvt_pk_fp8_f32 v144, v4, v10
	v_mul_f32_e32 v11, 0x43800000, v96
	v_mul_f32_e32 v4, 0x43800000, v88
	v_med3_f32 v10, v11, s0, v1
	v_med3_f32 v4, v4, s0, v1
	v_cvt_pk_fp8_f32 v144, v10, v4 op_sel:[0,0,1]
	v_mul_f32_e32 v4, 0x43800000, v100
	v_mul_f32_e32 v10, 0x43800000, v112
	v_med3_f32 v4, v4, s0, v1
	v_med3_f32 v10, v10, s0, v1
	v_mov_b32_e32 v145, v5
	v_cvt_pk_fp8_f32 v145, v4, v10
	v_mul_f32_e32 v11, 0x43800000, v128
	v_mul_f32_e32 v4, 0x43800000, v120
	v_med3_f32 v10, v11, s0, v1
	v_med3_f32 v4, v4, s0, v1
	v_cvt_pk_fp8_f32 v145, v10, v4 op_sel:[0,0,1]
	v_mul_f32_e32 v4, 0x43800000, v13
	v_mul_f32_e32 v10, 0x43800000, v21
	v_med3_f32 v4, v4, s0, v1
	v_med3_f32 v12, v10, s0, v1
	v_mov_b32_e32 v10, v5
	v_cvt_pk_fp8_f32 v10, v4, v12
	v_mul_f32_e32 v11, 0x43800000, v37
	v_mul_f32_e32 v4, 0x43800000, v29
	v_med3_f32 v11, v11, s0, v1
	v_med3_f32 v4, v4, s0, v1
	v_cvt_pk_fp8_f32 v10, v11, v4 op_sel:[0,0,1]
	v_mul_f32_e32 v4, 0x43800000, v45
	v_mul_f32_e32 v11, 0x43800000, v49
	v_med3_f32 v4, v4, s0, v1
	v_med3_f32 v13, v11, s0, v1
	v_mov_b32_e32 v11, v5
	v_cvt_pk_fp8_f32 v11, v4, v13
	v_mul_f32_e32 v12, 0x43800000, v65
	v_mul_f32_e32 v4, 0x43800000, v57
	v_med3_f32 v12, v12, s0, v1
	v_med3_f32 v4, v4, s0, v1
	v_cvt_pk_fp8_f32 v11, v12, v4 op_sel:[0,0,1]
	v_mul_f32_e32 v4, 0x43800000, v69
	v_mul_f32_e32 v12, 0x43800000, v81
	v_med3_f32 v4, v4, s0, v1
	v_med3_f32 v18, v12, s0, v1
	v_mov_b32_e32 v12, v5
	v_cvt_pk_fp8_f32 v12, v4, v18
	v_mul_f32_e32 v13, 0x43800000, v97
	v_mul_f32_e32 v4, 0x43800000, v89
	v_med3_f32 v13, v13, s0, v1
	v_med3_f32 v4, v4, s0, v1
	v_cvt_pk_fp8_f32 v12, v13, v4 op_sel:[0,0,1]
	v_mul_f32_e32 v4, 0x43800000, v101
	v_mul_f32_e32 v13, 0x43800000, v113
	v_med3_f32 v4, v4, s0, v1
	v_med3_f32 v19, v13, s0, v1
	v_mov_b32_e32 v13, v5
	v_cvt_pk_fp8_f32 v13, v4, v19
	v_mul_f32_e32 v18, 0x43800000, v129
	v_mul_f32_e32 v4, 0x43800000, v121
	v_med3_f32 v18, v18, s0, v1
	v_med3_f32 v4, v4, s0, v1
	v_cvt_pk_fp8_f32 v13, v18, v4 op_sel:[0,0,1]
	ds_write_b128 v166, v[134:137]
	ds_write_b128 v166, v[138:141] offset:272
	ds_write_b128 v166, v[142:145] offset:544
	ds_write_b128 v166, v[10:13] offset:816
	s_waitcnt lgkmcnt(0)
	s_barrier
	s_mov_b32 s1, 0xc00000
	v_add_co_u32_e32 v10, vcc, s1, v2
	s_mov_b32 s1, 0xc02000
	s_nop 0
	v_addc_co_u32_e32 v11, vcc, 0, v3, vcc
	v_add_co_u32_e32 v18, vcc, s1, v2
	s_mov_b32 s1, 0xc04000
	s_nop 0
	v_addc_co_u32_e32 v19, vcc, 0, v3, vcc
	v_add_co_u32_e32 v26, vcc, s1, v2
	s_mov_b32 s1, 0xc06000
	s_nop 0
	v_addc_co_u32_e32 v27, vcc, 0, v3, vcc
	v_add_co_u32_e32 v28, vcc, s1, v2
	s_mov_b32 s1, 0xc08000
	s_nop 0
	v_addc_co_u32_e32 v29, vcc, 0, v3, vcc
	v_add_co_u32_e32 v42, vcc, s1, v2
	s_mov_b32 s1, 0xc0a000
	s_nop 0
	v_addc_co_u32_e32 v43, vcc, 0, v3, vcc
	v_add_co_u32_e32 v46, vcc, s1, v2
	s_mov_b32 s1, 0xc0c000
	s_nop 0
	v_addc_co_u32_e32 v47, vcc, 0, v3, vcc
	v_add_co_u32_e32 v54, vcc, s1, v2
	s_mov_b32 s1, 0xc0e000
	s_nop 0
	v_addc_co_u32_e32 v55, vcc, 0, v3, vcc
	v_add_co_u32_e32 v56, vcc, s1, v2
	s_mov_b32 s1, 0xc10000
	s_nop 0
	v_addc_co_u32_e32 v57, vcc, 0, v3, vcc
	v_add_co_u32_e32 v66, vcc, s1, v2
	s_mov_b32 s1, 0xc12000
	s_nop 0
	v_addc_co_u32_e32 v67, vcc, 0, v3, vcc
	v_add_co_u32_e32 v78, vcc, s1, v2
	s_mov_b32 s1, 0xc14000
	s_nop 0
	v_addc_co_u32_e32 v79, vcc, 0, v3, vcc
	v_add_co_u32_e32 v86, vcc, s1, v2
	s_mov_b32 s1, 0xc16000
	s_nop 0
	v_addc_co_u32_e32 v87, vcc, 0, v3, vcc
	v_add_co_u32_e32 v88, vcc, s1, v2
	s_mov_b32 s1, 0xc18000
	s_nop 0
	v_addc_co_u32_e32 v89, vcc, 0, v3, vcc
	v_add_co_u32_e32 v98, vcc, s1, v2
	s_mov_b32 s1, 0xc1a000
	s_nop 0
	v_addc_co_u32_e32 v99, vcc, 0, v3, vcc
	v_add_co_u32_e32 v110, vcc, s1, v2
	s_mov_b32 s1, 0xc1c000
	s_nop 0
	v_addc_co_u32_e32 v111, vcc, 0, v3, vcc
	v_add_co_u32_e32 v118, vcc, s1, v2
	s_mov_b32 s1, 0xc1e000
	s_nop 0
	v_addc_co_u32_e32 v119, vcc, 0, v3, vcc
	v_add_co_u32_e32 v120, vcc, s1, v2
	global_load_dwordx4 v[10:13], v[10:11], off sc0 nt
	s_nop 0
	global_load_dwordx4 v[18:21], v[18:19], off sc0 nt
	v_addc_co_u32_e32 v121, vcc, 0, v3, vcc
	global_load_dwordx4 v[34:37], v[26:27], off sc0 nt
	s_nop 0
	global_load_dwordx4 v[26:29], v[28:29], off sc0 nt
	s_nop 0
	global_load_dwordx4 v[42:45], v[42:43], off sc0 nt
	s_nop 0
	global_load_dwordx4 v[46:49], v[46:47], off sc0 nt
	s_nop 0
	global_load_dwordx4 v[62:65], v[54:55], off sc0 nt
	s_nop 0
	global_load_dwordx4 v[54:57], v[56:57], off sc0 nt
	s_nop 0
	global_load_dwordx4 v[66:69], v[66:67], off sc0 nt
	s_nop 0
	global_load_dwordx4 v[78:81], v[78:79], off sc0 nt
	s_nop 0
	global_load_dwordx4 v[94:97], v[86:87], off sc0 nt
	s_nop 0
	global_load_dwordx4 v[86:89], v[88:89], off sc0 nt
	s_nop 0
	global_load_dwordx4 v[98:101], v[98:99], off sc0 nt
	s_nop 0
	global_load_dwordx4 v[110:113], v[110:111], off sc0 nt
	s_nop 0
	global_load_dwordx4 v[126:129], v[118:119], off sc0 nt
	s_nop 0
	global_load_dwordx4 v[118:121], v[120:121], off sc0 nt
	ds_read_b128 v[134:137], v154
	ds_read_b128 v[138:141], v156
	ds_read_b128 v[142:145], v158
	ds_read_b128 v[146:149], v162
	s_waitcnt lgkmcnt(3)
	global_store_dwordx4 v[150:151], v[134:137], off offset:1024 nt
	s_waitcnt lgkmcnt(2)
	global_store_dwordx4 v[152:153], v[138:141], off offset:1024 nt
	s_waitcnt lgkmcnt(1)
	global_store_dwordx4 v[160:161], v[142:145], off offset:1024 nt
	s_waitcnt lgkmcnt(0)
	global_store_dwordx4 v[164:165], v[146:149], off offset:1024 nt
	s_waitcnt vmcnt(39)
	v_mul_f32_e32 v4, 0x43800000, v6
	s_waitcnt vmcnt(38)
	v_mul_f32_e32 v6, 0x43800000, v14
	v_med3_f32 v4, v4, s0, v1
	v_med3_f32 v6, v6, s0, v1
	v_mov_b32_e32 v134, v5
	v_cvt_pk_fp8_f32 v134, v4, v6
	s_waitcnt vmcnt(37)
	v_mul_f32_e32 v14, 0x43800000, v30
	s_waitcnt vmcnt(36)
	v_mul_f32_e32 v4, 0x43800000, v22
	v_med3_f32 v6, v14, s0, v1
	v_med3_f32 v4, v4, s0, v1
	v_cvt_pk_fp8_f32 v134, v6, v4 op_sel:[0,0,1]
	s_waitcnt vmcnt(35)
	v_mul_f32_e32 v4, 0x43800000, v38
	s_waitcnt vmcnt(34)
	v_mul_f32_e32 v6, 0x43800000, v50
	v_med3_f32 v4, v4, s0, v1
	v_med3_f32 v6, v6, s0, v1
	v_mov_b32_e32 v135, v5
	v_cvt_pk_fp8_f32 v135, v4, v6
	s_waitcnt vmcnt(33)
	v_mul_f32_e32 v14, 0x43800000, v70
	s_waitcnt vmcnt(32)
	v_mul_f32_e32 v4, 0x43800000, v58
	v_med3_f32 v6, v14, s0, v1
	v_med3_f32 v4, v4, s0, v1
	v_cvt_pk_fp8_f32 v135, v6, v4 op_sel:[0,0,1]
	s_waitcnt vmcnt(31)
	v_mul_f32_e32 v4, 0x43800000, v74
	s_waitcnt vmcnt(30)
	v_mul_f32_e32 v6, 0x43800000, v82
	v_med3_f32 v4, v4, s0, v1
	v_med3_f32 v6, v6, s0, v1
	v_mov_b32_e32 v136, v5
	v_cvt_pk_fp8_f32 v136, v4, v6
	s_waitcnt vmcnt(29)
	v_mul_f32_e32 v14, 0x43800000, v102
	s_waitcnt vmcnt(28)
	v_mul_f32_e32 v4, 0x43800000, v90
	v_med3_f32 v6, v14, s0, v1
	v_med3_f32 v4, v4, s0, v1
	v_cvt_pk_fp8_f32 v136, v6, v4 op_sel:[0,0,1]
	s_waitcnt vmcnt(27)
	v_mul_f32_e32 v4, 0x43800000, v106
	s_waitcnt vmcnt(26)
	v_mul_f32_e32 v6, 0x43800000, v114
	v_med3_f32 v4, v4, s0, v1
	v_med3_f32 v6, v6, s0, v1
	v_mov_b32_e32 v137, v5
	v_cvt_pk_fp8_f32 v137, v4, v6
	s_waitcnt vmcnt(25)
	v_mul_f32_e32 v14, 0x43800000, v130
	s_waitcnt vmcnt(24)
	v_mul_f32_e32 v4, 0x43800000, v122
	v_med3_f32 v6, v14, s0, v1
	v_med3_f32 v4, v4, s0, v1
	v_cvt_pk_fp8_f32 v137, v6, v4 op_sel:[0,0,1]
	v_mul_f32_e32 v4, 0x43800000, v7
	v_mul_f32_e32 v6, 0x43800000, v15
	v_med3_f32 v4, v4, s0, v1
	v_med3_f32 v6, v6, s0, v1
	v_mov_b32_e32 v138, v5
	v_cvt_pk_fp8_f32 v138, v4, v6
	v_mul_f32_e32 v7, 0x43800000, v31
	v_mul_f32_e32 v4, 0x43800000, v23
	v_med3_f32 v6, v7, s0, v1
	v_med3_f32 v4, v4, s0, v1
	v_cvt_pk_fp8_f32 v138, v6, v4 op_sel:[0,0,1]
	v_mul_f32_e32 v4, 0x43800000, v39
	v_mul_f32_e32 v6, 0x43800000, v51
	v_med3_f32 v4, v4, s0, v1
	v_med3_f32 v6, v6, s0, v1
	v_mov_b32_e32 v139, v5
	v_cvt_pk_fp8_f32 v139, v4, v6
	v_mul_f32_e32 v7, 0x43800000, v71
	v_mul_f32_e32 v4, 0x43800000, v59
	v_med3_f32 v6, v7, s0, v1
	v_med3_f32 v4, v4, s0, v1
	v_cvt_pk_fp8_f32 v139, v6, v4 op_sel:[0,0,1]
	v_mul_f32_e32 v4, 0x43800000, v75
	v_mul_f32_e32 v6, 0x43800000, v83
	v_med3_f32 v4, v4, s0, v1
	v_med3_f32 v6, v6, s0, v1
	v_mov_b32_e32 v140, v5
	v_cvt_pk_fp8_f32 v140, v4, v6
	v_mul_f32_e32 v7, 0x43800000, v103
	v_mul_f32_e32 v4, 0x43800000, v91
	v_med3_f32 v6, v7, s0, v1
	v_med3_f32 v4, v4, s0, v1
	v_cvt_pk_fp8_f32 v140, v6, v4 op_sel:[0,0,1]
	v_mul_f32_e32 v4, 0x43800000, v107
	v_mul_f32_e32 v6, 0x43800000, v115
	v_med3_f32 v4, v4, s0, v1
	v_med3_f32 v6, v6, s0, v1
	v_mov_b32_e32 v141, v5
	v_cvt_pk_fp8_f32 v141, v4, v6
	v_mul_f32_e32 v7, 0x43800000, v131
	v_mul_f32_e32 v4, 0x43800000, v123
	v_med3_f32 v6, v7, s0, v1
	v_med3_f32 v4, v4, s0, v1
	v_cvt_pk_fp8_f32 v141, v6, v4 op_sel:[0,0,1]
	v_mul_f32_e32 v4, 0x43800000, v8
	v_mul_f32_e32 v6, 0x43800000, v16
	v_med3_f32 v4, v4, s0, v1
	v_med3_f32 v6, v6, s0, v1
	v_mov_b32_e32 v142, v5
	v_cvt_pk_fp8_f32 v142, v4, v6
	v_mul_f32_e32 v7, 0x43800000, v32
	v_mul_f32_e32 v4, 0x43800000, v24
	v_med3_f32 v6, v7, s0, v1
	v_med3_f32 v4, v4, s0, v1
	v_cvt_pk_fp8_f32 v142, v6, v4 op_sel:[0,0,1]
	v_mul_f32_e32 v4, 0x43800000, v40
	v_mul_f32_e32 v6, 0x43800000, v52
	v_med3_f32 v4, v4, s0, v1
	v_med3_f32 v6, v6, s0, v1
	v_mov_b32_e32 v143, v5
	v_cvt_pk_fp8_f32 v143, v4, v6
	v_mul_f32_e32 v7, 0x43800000, v72
	v_mul_f32_e32 v4, 0x43800000, v60
	v_med3_f32 v6, v7, s0, v1
	v_med3_f32 v4, v4, s0, v1
	v_cvt_pk_fp8_f32 v143, v6, v4 op_sel:[0,0,1]
	v_mul_f32_e32 v4, 0x43800000, v76
	v_mul_f32_e32 v6, 0x43800000, v84
	v_med3_f32 v4, v4, s0, v1
	v_med3_f32 v6, v6, s0, v1
	v_mov_b32_e32 v144, v5
	v_cvt_pk_fp8_f32 v144, v4, v6
	v_mul_f32_e32 v7, 0x43800000, v104
	v_mul_f32_e32 v4, 0x43800000, v92
	v_med3_f32 v6, v7, s0, v1
	v_med3_f32 v4, v4, s0, v1
	v_cvt_pk_fp8_f32 v144, v6, v4 op_sel:[0,0,1]
	v_mul_f32_e32 v4, 0x43800000, v108
	v_mul_f32_e32 v6, 0x43800000, v116
	v_med3_f32 v4, v4, s0, v1
	v_med3_f32 v6, v6, s0, v1
	v_mov_b32_e32 v145, v5
	v_cvt_pk_fp8_f32 v145, v4, v6
	v_mul_f32_e32 v7, 0x43800000, v132
	v_mul_f32_e32 v4, 0x43800000, v124
	v_med3_f32 v6, v7, s0, v1
	v_med3_f32 v4, v4, s0, v1
	v_cvt_pk_fp8_f32 v145, v6, v4 op_sel:[0,0,1]
	v_mul_f32_e32 v4, 0x43800000, v9
	v_mul_f32_e32 v6, 0x43800000, v17
	v_med3_f32 v4, v4, s0, v1
	v_med3_f32 v8, v6, s0, v1
	v_mov_b32_e32 v6, v5
	v_cvt_pk_fp8_f32 v6, v4, v8
	v_mul_f32_e32 v7, 0x43800000, v33
	v_mul_f32_e32 v4, 0x43800000, v25
	v_med3_f32 v7, v7, s0, v1
	v_med3_f32 v4, v4, s0, v1
	v_cvt_pk_fp8_f32 v6, v7, v4 op_sel:[0,0,1]
	v_mul_f32_e32 v4, 0x43800000, v41
	v_mul_f32_e32 v7, 0x43800000, v53
	v_med3_f32 v4, v4, s0, v1
	v_med3_f32 v9, v7, s0, v1
	v_mov_b32_e32 v7, v5
	v_cvt_pk_fp8_f32 v7, v4, v9
	v_mul_f32_e32 v8, 0x43800000, v73
	v_mul_f32_e32 v4, 0x43800000, v61
	v_med3_f32 v8, v8, s0, v1
	v_med3_f32 v4, v4, s0, v1
	v_cvt_pk_fp8_f32 v7, v8, v4 op_sel:[0,0,1]
	v_mul_f32_e32 v4, 0x43800000, v77
	v_mul_f32_e32 v8, 0x43800000, v85
	v_med3_f32 v4, v4, s0, v1
	v_med3_f32 v14, v8, s0, v1
	v_mov_b32_e32 v8, v5
	v_cvt_pk_fp8_f32 v8, v4, v14
	v_mul_f32_e32 v9, 0x43800000, v105
	v_mul_f32_e32 v4, 0x43800000, v93
	v_med3_f32 v9, v9, s0, v1
	v_med3_f32 v4, v4, s0, v1
	v_cvt_pk_fp8_f32 v8, v9, v4 op_sel:[0,0,1]
	v_mul_f32_e32 v4, 0x43800000, v109
	v_mul_f32_e32 v9, 0x43800000, v117
	v_med3_f32 v4, v4, s0, v1
	v_med3_f32 v15, v9, s0, v1
	v_mov_b32_e32 v9, v5
	v_cvt_pk_fp8_f32 v9, v4, v15
	v_mul_f32_e32 v14, 0x43800000, v133
	v_mul_f32_e32 v4, 0x43800000, v125
	v_med3_f32 v14, v14, s0, v1
	v_med3_f32 v4, v4, s0, v1
	v_cvt_pk_fp8_f32 v9, v14, v4 op_sel:[0,0,1]
	ds_write_b128 v166, v[134:137] offset:34816
	ds_write_b128 v166, v[138:141] offset:35088
	ds_write_b128 v166, v[142:145] offset:35360
	ds_write_b128 v166, v[6:9] offset:35632
	s_waitcnt lgkmcnt(0)
	s_barrier
	s_mov_b32 s1, 0xe00000
	v_add_co_u32_e32 v6, vcc, s1, v2
	s_mov_b32 s1, 0xe02000
	s_nop 0
	v_addc_co_u32_e32 v7, vcc, 0, v3, vcc
	v_add_co_u32_e32 v14, vcc, s1, v2
	s_mov_b32 s1, 0xe04000
	s_nop 0
	v_addc_co_u32_e32 v15, vcc, 0, v3, vcc
	v_add_co_u32_e32 v22, vcc, s1, v2
	s_mov_b32 s1, 0xe06000
	s_nop 0
	v_addc_co_u32_e32 v23, vcc, 0, v3, vcc
	v_add_co_u32_e32 v24, vcc, s1, v2
	s_mov_b32 s1, 0xe08000
	s_nop 0
	v_addc_co_u32_e32 v25, vcc, 0, v3, vcc
	v_add_co_u32_e32 v38, vcc, s1, v2
	s_mov_b32 s1, 0xe0a000
	s_nop 0
	v_addc_co_u32_e32 v39, vcc, 0, v3, vcc
	v_add_co_u32_e32 v50, vcc, s1, v2
	s_mov_b32 s1, 0xe0c000
	s_nop 0
	v_addc_co_u32_e32 v51, vcc, 0, v3, vcc
	v_add_co_u32_e32 v58, vcc, s1, v2
	s_mov_b32 s1, 0xe0e000
	s_nop 0
	v_addc_co_u32_e32 v59, vcc, 0, v3, vcc
	v_add_co_u32_e32 v60, vcc, s1, v2
	s_mov_b32 s1, 0xe10000
	s_nop 0
	v_addc_co_u32_e32 v61, vcc, 0, v3, vcc
	v_add_co_u32_e32 v74, vcc, s1, v2
	s_mov_b32 s1, 0xe12000
	s_nop 0
	v_addc_co_u32_e32 v75, vcc, 0, v3, vcc
	v_add_co_u32_e32 v82, vcc, s1, v2
	s_mov_b32 s1, 0xe14000
	s_nop 0
	v_addc_co_u32_e32 v83, vcc, 0, v3, vcc
	v_add_co_u32_e32 v90, vcc, s1, v2
	s_mov_b32 s1, 0xe16000
	s_nop 0
	v_addc_co_u32_e32 v91, vcc, 0, v3, vcc
	v_add_co_u32_e32 v92, vcc, s1, v2
	s_mov_b32 s1, 0xe18000
	s_nop 0
	v_addc_co_u32_e32 v93, vcc, 0, v3, vcc
	v_add_co_u32_e32 v106, vcc, s1, v2
	s_mov_b32 s1, 0xe1a000
	s_nop 0
	v_addc_co_u32_e32 v107, vcc, 0, v3, vcc
	v_add_co_u32_e32 v114, vcc, s1, v2
	s_mov_b32 s1, 0xe1c000
	s_nop 0
	v_addc_co_u32_e32 v115, vcc, 0, v3, vcc
	v_add_co_u32_e32 v122, vcc, s1, v2
	s_mov_b32 s1, 0xe1e000
	s_nop 0
	v_addc_co_u32_e32 v123, vcc, 0, v3, vcc
	v_add_co_u32_e32 v2, vcc, s1, v2
	global_load_dwordx4 v[6:9], v[6:7], off sc0 nt
	s_nop 0
	global_load_dwordx4 v[14:17], v[14:15], off sc0 nt
	s_nop 0
	global_load_dwordx4 v[30:33], v[22:23], off sc0 nt
	s_nop 0
	global_load_dwordx4 v[22:25], v[24:25], off sc0 nt
	s_nop 0
	global_load_dwordx4 v[38:41], v[38:39], off sc0 nt
	s_nop 0
	global_load_dwordx4 v[50:53], v[50:51], off sc0 nt
	s_nop 0
	global_load_dwordx4 v[70:73], v[58:59], off sc0 nt
	s_nop 0
	global_load_dwordx4 v[58:61], v[60:61], off sc0 nt
	s_nop 0
	global_load_dwordx4 v[74:77], v[74:75], off sc0 nt
	s_nop 0
	global_load_dwordx4 v[82:85], v[82:83], off sc0 nt
	s_nop 0
	global_load_dwordx4 v[102:105], v[90:91], off sc0 nt
	s_nop 0
	global_load_dwordx4 v[90:93], v[92:93], off sc0 nt
	s_nop 0
	global_load_dwordx4 v[106:109], v[106:107], off sc0 nt
	s_nop 0
	global_load_dwordx4 v[114:117], v[114:115], off sc0 nt
	v_addc_co_u32_e32 v3, vcc, 0, v3, vcc
	global_load_dwordx4 v[130:133], v[122:123], off sc0 nt
	s_nop 0
	global_load_dwordx4 v[122:125], v[2:3], off sc0 nt
	ds_read_b128 v[134:137], v154 offset:34816
	ds_read_b128 v[138:141], v156 offset:34816
	ds_read_b128 v[142:145], v158 offset:34816
	ds_read_b128 v[146:149], v162 offset:34816
	s_waitcnt lgkmcnt(3)
	global_store_dwordx4 v[150:151], v[134:137], off offset:1280 nt
	s_waitcnt lgkmcnt(2)
	global_store_dwordx4 v[152:153], v[138:141], off offset:1280 nt
	s_waitcnt lgkmcnt(1)
	global_store_dwordx4 v[160:161], v[142:145], off offset:1280 nt
	s_waitcnt lgkmcnt(0)
	global_store_dwordx4 v[164:165], v[146:149], off offset:1280 nt
	s_waitcnt vmcnt(39)
	v_mul_f32_e32 v2, 0x43800000, v10
	s_waitcnt vmcnt(38)
	v_mul_f32_e32 v3, 0x43800000, v18
	v_med3_f32 v2, v2, s0, v1
	v_med3_f32 v3, v3, s0, v1
	v_mov_b32_e32 v134, v5
	v_cvt_pk_fp8_f32 v134, v2, v3
	s_waitcnt vmcnt(37)
	v_mul_f32_e32 v4, 0x43800000, v34
	s_waitcnt vmcnt(36)
	v_mul_f32_e32 v2, 0x43800000, v26
	v_med3_f32 v3, v4, s0, v1
	v_med3_f32 v2, v2, s0, v1
	v_cvt_pk_fp8_f32 v134, v3, v2 op_sel:[0,0,1]
	s_waitcnt vmcnt(35)
	v_mul_f32_e32 v2, 0x43800000, v42
	s_waitcnt vmcnt(34)
	v_mul_f32_e32 v3, 0x43800000, v46
	v_med3_f32 v2, v2, s0, v1
	v_med3_f32 v3, v3, s0, v1
	v_mov_b32_e32 v135, v5
	v_cvt_pk_fp8_f32 v135, v2, v3
	s_waitcnt vmcnt(33)
	v_mul_f32_e32 v4, 0x43800000, v62
	s_waitcnt vmcnt(32)
	v_mul_f32_e32 v2, 0x43800000, v54
	v_med3_f32 v3, v4, s0, v1
	v_med3_f32 v2, v2, s0, v1
	v_cvt_pk_fp8_f32 v135, v3, v2 op_sel:[0,0,1]
	s_waitcnt vmcnt(31)
	v_mul_f32_e32 v2, 0x43800000, v66
	s_waitcnt vmcnt(30)
	v_mul_f32_e32 v3, 0x43800000, v78
	v_med3_f32 v2, v2, s0, v1
	v_med3_f32 v3, v3, s0, v1
	v_mov_b32_e32 v136, v5
	v_cvt_pk_fp8_f32 v136, v2, v3
	s_waitcnt vmcnt(29)
	v_mul_f32_e32 v4, 0x43800000, v94
	s_waitcnt vmcnt(28)
	v_mul_f32_e32 v2, 0x43800000, v86
	v_med3_f32 v3, v4, s0, v1
	v_med3_f32 v2, v2, s0, v1
	v_cvt_pk_fp8_f32 v136, v3, v2 op_sel:[0,0,1]
	s_waitcnt vmcnt(27)
	v_mul_f32_e32 v2, 0x43800000, v98
	s_waitcnt vmcnt(26)
	v_mul_f32_e32 v3, 0x43800000, v110
	v_med3_f32 v2, v2, s0, v1
	v_med3_f32 v3, v3, s0, v1
	v_mov_b32_e32 v137, v5
	v_cvt_pk_fp8_f32 v137, v2, v3
	s_waitcnt vmcnt(25)
	v_mul_f32_e32 v4, 0x43800000, v126
	s_waitcnt vmcnt(24)
	v_mul_f32_e32 v2, 0x43800000, v118
	v_med3_f32 v3, v4, s0, v1
	v_med3_f32 v2, v2, s0, v1
	v_cvt_pk_fp8_f32 v137, v3, v2 op_sel:[0,0,1]
	v_mul_f32_e32 v2, 0x43800000, v11
	v_mul_f32_e32 v3, 0x43800000, v19
	v_med3_f32 v2, v2, s0, v1
	v_med3_f32 v3, v3, s0, v1
	v_mov_b32_e32 v138, v5
	v_cvt_pk_fp8_f32 v138, v2, v3
	v_mul_f32_e32 v4, 0x43800000, v35
	v_mul_f32_e32 v2, 0x43800000, v27
	v_med3_f32 v3, v4, s0, v1
	v_med3_f32 v2, v2, s0, v1
	v_cvt_pk_fp8_f32 v138, v3, v2 op_sel:[0,0,1]
	v_mul_f32_e32 v2, 0x43800000, v43
	v_mul_f32_e32 v3, 0x43800000, v47
	v_med3_f32 v2, v2, s0, v1
	v_med3_f32 v3, v3, s0, v1
	v_mov_b32_e32 v139, v5
	v_cvt_pk_fp8_f32 v139, v2, v3
	v_mul_f32_e32 v4, 0x43800000, v63
	v_mul_f32_e32 v2, 0x43800000, v55
	v_med3_f32 v3, v4, s0, v1
	v_med3_f32 v2, v2, s0, v1
	v_cvt_pk_fp8_f32 v139, v3, v2 op_sel:[0,0,1]
	v_mul_f32_e32 v2, 0x43800000, v67
	v_mul_f32_e32 v3, 0x43800000, v79
	v_med3_f32 v2, v2, s0, v1
	v_med3_f32 v3, v3, s0, v1
	v_mov_b32_e32 v140, v5
	v_cvt_pk_fp8_f32 v140, v2, v3
	v_mul_f32_e32 v4, 0x43800000, v95
	v_mul_f32_e32 v2, 0x43800000, v87
	v_med3_f32 v3, v4, s0, v1
	v_med3_f32 v2, v2, s0, v1
	v_cvt_pk_fp8_f32 v140, v3, v2 op_sel:[0,0,1]
	v_mul_f32_e32 v2, 0x43800000, v99
	v_mul_f32_e32 v3, 0x43800000, v111
	v_med3_f32 v2, v2, s0, v1
	v_med3_f32 v3, v3, s0, v1
	v_mov_b32_e32 v141, v5
	v_cvt_pk_fp8_f32 v141, v2, v3
	v_mul_f32_e32 v4, 0x43800000, v127
	v_mul_f32_e32 v2, 0x43800000, v119
	v_med3_f32 v3, v4, s0, v1
	v_med3_f32 v2, v2, s0, v1
	v_cvt_pk_fp8_f32 v141, v3, v2 op_sel:[0,0,1]
	v_mul_f32_e32 v2, 0x43800000, v12
	v_mul_f32_e32 v3, 0x43800000, v20
	v_med3_f32 v2, v2, s0, v1
	v_med3_f32 v3, v3, s0, v1
	v_mov_b32_e32 v142, v5
	v_cvt_pk_fp8_f32 v142, v2, v3
	v_mul_f32_e32 v4, 0x43800000, v36
	v_mul_f32_e32 v2, 0x43800000, v28
	v_med3_f32 v3, v4, s0, v1
	v_med3_f32 v2, v2, s0, v1
	v_cvt_pk_fp8_f32 v142, v3, v2 op_sel:[0,0,1]
	v_mul_f32_e32 v2, 0x43800000, v44
	v_mul_f32_e32 v3, 0x43800000, v48
	v_med3_f32 v2, v2, s0, v1
	v_med3_f32 v3, v3, s0, v1
	v_mov_b32_e32 v143, v5
	v_cvt_pk_fp8_f32 v143, v2, v3
	v_mul_f32_e32 v4, 0x43800000, v64
	v_mul_f32_e32 v2, 0x43800000, v56
	v_med3_f32 v3, v4, s0, v1
	v_med3_f32 v2, v2, s0, v1
	v_cvt_pk_fp8_f32 v143, v3, v2 op_sel:[0,0,1]
	v_mul_f32_e32 v2, 0x43800000, v68
	v_mul_f32_e32 v3, 0x43800000, v80
	v_med3_f32 v2, v2, s0, v1
	v_med3_f32 v3, v3, s0, v1
	v_mov_b32_e32 v144, v5
	v_cvt_pk_fp8_f32 v144, v2, v3
	v_mul_f32_e32 v4, 0x43800000, v96
	v_mul_f32_e32 v2, 0x43800000, v88
	v_med3_f32 v3, v4, s0, v1
	v_med3_f32 v2, v2, s0, v1
	v_cvt_pk_fp8_f32 v144, v3, v2 op_sel:[0,0,1]
	v_mul_f32_e32 v2, 0x43800000, v100
	v_mul_f32_e32 v3, 0x43800000, v112
	v_med3_f32 v2, v2, s0, v1
	v_med3_f32 v3, v3, s0, v1
	v_mov_b32_e32 v145, v5
	v_cvt_pk_fp8_f32 v145, v2, v3
	v_mul_f32_e32 v4, 0x43800000, v128
	v_mul_f32_e32 v2, 0x43800000, v120
	v_med3_f32 v3, v4, s0, v1
	v_med3_f32 v2, v2, s0, v1
	v_cvt_pk_fp8_f32 v145, v3, v2 op_sel:[0,0,1]
	v_mul_f32_e32 v2, 0x43800000, v13
	v_mul_f32_e32 v3, 0x43800000, v21
	v_med3_f32 v2, v2, s0, v1
	v_med3_f32 v3, v3, s0, v1
	v_mov_b32_e32 v10, v5
	v_cvt_pk_fp8_f32 v10, v2, v3
	v_mul_f32_e32 v4, 0x43800000, v37
	v_mul_f32_e32 v2, 0x43800000, v29
	v_med3_f32 v3, v4, s0, v1
	v_med3_f32 v2, v2, s0, v1
	v_cvt_pk_fp8_f32 v10, v3, v2 op_sel:[0,0,1]
	v_mul_f32_e32 v2, 0x43800000, v45
	v_mul_f32_e32 v3, 0x43800000, v49
	v_med3_f32 v2, v2, s0, v1
	v_med3_f32 v3, v3, s0, v1
	v_mov_b32_e32 v11, v5
	v_cvt_pk_fp8_f32 v11, v2, v3
	v_mul_f32_e32 v4, 0x43800000, v65
	v_mul_f32_e32 v2, 0x43800000, v57
	v_med3_f32 v3, v4, s0, v1
	v_med3_f32 v2, v2, s0, v1
	v_cvt_pk_fp8_f32 v11, v3, v2 op_sel:[0,0,1]
	v_mul_f32_e32 v2, 0x43800000, v69
	v_mul_f32_e32 v3, 0x43800000, v81
	v_med3_f32 v2, v2, s0, v1
	v_med3_f32 v3, v3, s0, v1
	v_mov_b32_e32 v12, v5
	v_cvt_pk_fp8_f32 v12, v2, v3
	v_mul_f32_e32 v4, 0x43800000, v97
	v_mul_f32_e32 v2, 0x43800000, v89
	v_med3_f32 v3, v4, s0, v1
	v_med3_f32 v2, v2, s0, v1
	v_cvt_pk_fp8_f32 v12, v3, v2 op_sel:[0,0,1]
	v_mul_f32_e32 v2, 0x43800000, v101
	v_mul_f32_e32 v3, 0x43800000, v113
	v_med3_f32 v2, v2, s0, v1
	v_med3_f32 v3, v3, s0, v1
	v_mov_b32_e32 v13, v5
	v_cvt_pk_fp8_f32 v13, v2, v3
	v_mul_f32_e32 v4, 0x43800000, v129
	v_mul_f32_e32 v2, 0x43800000, v121
	v_med3_f32 v3, v4, s0, v1
	v_med3_f32 v2, v2, s0, v1
	v_cvt_pk_fp8_f32 v13, v3, v2 op_sel:[0,0,1]
	ds_write_b128 v166, v[134:137]
	ds_write_b128 v166, v[138:141] offset:272
	ds_write_b128 v166, v[142:145] offset:544
	ds_write_b128 v166, v[10:13] offset:816
	s_waitcnt lgkmcnt(0)
	s_barrier
	ds_read_b128 v[10:13], v154
	ds_read_b128 v[18:21], v156
	ds_read_b128 v[26:29], v158
	ds_read_b128 v[34:37], v162
	s_waitcnt lgkmcnt(3)
	global_store_dwordx4 v[150:151], v[10:13], off offset:1536 nt
	s_waitcnt lgkmcnt(2)
	global_store_dwordx4 v[152:153], v[18:21], off offset:1536 nt
	s_waitcnt lgkmcnt(1)
	global_store_dwordx4 v[160:161], v[26:29], off offset:1536 nt
	s_waitcnt lgkmcnt(0)
	global_store_dwordx4 v[164:165], v[34:37], off offset:1536 nt
	s_waitcnt vmcnt(23)
	v_mul_f32_e32 v2, 0x43800000, v6
	s_waitcnt vmcnt(22)
	v_mul_f32_e32 v3, 0x43800000, v14
	v_med3_f32 v2, v2, s0, v1
	v_med3_f32 v3, v3, s0, v1
	v_mov_b32_e32 v10, v5
	v_cvt_pk_fp8_f32 v10, v2, v3
	s_waitcnt vmcnt(21)
	v_mul_f32_e32 v4, 0x43800000, v30
	s_waitcnt vmcnt(20)
	v_mul_f32_e32 v2, 0x43800000, v22
	v_med3_f32 v3, v4, s0, v1
	v_med3_f32 v2, v2, s0, v1
	v_cvt_pk_fp8_f32 v10, v3, v2 op_sel:[0,0,1]
	s_waitcnt vmcnt(19)
	v_mul_f32_e32 v2, 0x43800000, v38
	s_waitcnt vmcnt(18)
	v_mul_f32_e32 v3, 0x43800000, v50
	v_med3_f32 v2, v2, s0, v1
	v_med3_f32 v3, v3, s0, v1
	v_mov_b32_e32 v11, v5
	v_cvt_pk_fp8_f32 v11, v2, v3
	s_waitcnt vmcnt(17)
	v_mul_f32_e32 v4, 0x43800000, v70
	s_waitcnt vmcnt(16)
	v_mul_f32_e32 v2, 0x43800000, v58
	v_med3_f32 v3, v4, s0, v1
	v_med3_f32 v2, v2, s0, v1
	v_cvt_pk_fp8_f32 v11, v3, v2 op_sel:[0,0,1]
	s_waitcnt vmcnt(15)
	v_mul_f32_e32 v2, 0x43800000, v74
	s_waitcnt vmcnt(14)
	v_mul_f32_e32 v3, 0x43800000, v82
	v_med3_f32 v2, v2, s0, v1
	v_med3_f32 v3, v3, s0, v1
	v_mov_b32_e32 v12, v5
	v_cvt_pk_fp8_f32 v12, v2, v3
	s_waitcnt vmcnt(13)
	v_mul_f32_e32 v4, 0x43800000, v102
	s_waitcnt vmcnt(12)
	v_mul_f32_e32 v2, 0x43800000, v90
	v_med3_f32 v3, v4, s0, v1
	v_med3_f32 v2, v2, s0, v1
	v_cvt_pk_fp8_f32 v12, v3, v2 op_sel:[0,0,1]
	s_waitcnt vmcnt(11)
	v_mul_f32_e32 v2, 0x43800000, v106
	s_waitcnt vmcnt(10)
	v_mul_f32_e32 v3, 0x43800000, v114
	v_med3_f32 v2, v2, s0, v1
	v_med3_f32 v3, v3, s0, v1
	v_mov_b32_e32 v13, v5
	v_cvt_pk_fp8_f32 v13, v2, v3
	s_waitcnt vmcnt(9)
	v_mul_f32_e32 v4, 0x43800000, v130
	s_waitcnt vmcnt(8)
	v_mul_f32_e32 v2, 0x43800000, v122
	v_med3_f32 v3, v4, s0, v1
	v_med3_f32 v2, v2, s0, v1
	v_cvt_pk_fp8_f32 v13, v3, v2 op_sel:[0,0,1]
	v_mul_f32_e32 v2, 0x43800000, v7
	v_mul_f32_e32 v3, 0x43800000, v15
	v_med3_f32 v2, v2, s0, v1
	v_med3_f32 v3, v3, s0, v1
	v_mov_b32_e32 v18, v5
	v_cvt_pk_fp8_f32 v18, v2, v3
	v_mul_f32_e32 v4, 0x43800000, v31
	v_mul_f32_e32 v2, 0x43800000, v23
	v_med3_f32 v3, v4, s0, v1
	v_med3_f32 v2, v2, s0, v1
	v_cvt_pk_fp8_f32 v18, v3, v2 op_sel:[0,0,1]
	v_mul_f32_e32 v2, 0x43800000, v39
	v_mul_f32_e32 v3, 0x43800000, v51
	v_med3_f32 v2, v2, s0, v1
	v_med3_f32 v3, v3, s0, v1
	v_mov_b32_e32 v19, v5
	v_cvt_pk_fp8_f32 v19, v2, v3
	v_mul_f32_e32 v4, 0x43800000, v71
	v_mul_f32_e32 v2, 0x43800000, v59
	v_med3_f32 v3, v4, s0, v1
	v_med3_f32 v2, v2, s0, v1
	v_cvt_pk_fp8_f32 v19, v3, v2 op_sel:[0,0,1]
	v_mul_f32_e32 v2, 0x43800000, v75
	v_mul_f32_e32 v3, 0x43800000, v83
	v_med3_f32 v2, v2, s0, v1
	v_med3_f32 v3, v3, s0, v1
	v_mov_b32_e32 v20, v5
	v_cvt_pk_fp8_f32 v20, v2, v3
	v_mul_f32_e32 v4, 0x43800000, v103
	v_mul_f32_e32 v2, 0x43800000, v91
	v_med3_f32 v3, v4, s0, v1
	v_med3_f32 v2, v2, s0, v1
	v_cvt_pk_fp8_f32 v20, v3, v2 op_sel:[0,0,1]
	v_mul_f32_e32 v2, 0x43800000, v107
	v_mul_f32_e32 v3, 0x43800000, v115
	v_med3_f32 v2, v2, s0, v1
	v_med3_f32 v3, v3, s0, v1
	v_mov_b32_e32 v21, v5
	v_cvt_pk_fp8_f32 v21, v2, v3
	v_mul_f32_e32 v4, 0x43800000, v131
	v_mul_f32_e32 v2, 0x43800000, v123
	v_med3_f32 v3, v4, s0, v1
	v_med3_f32 v2, v2, s0, v1
	v_cvt_pk_fp8_f32 v21, v3, v2 op_sel:[0,0,1]
	v_mul_f32_e32 v2, 0x43800000, v8
	v_mul_f32_e32 v3, 0x43800000, v16
	v_med3_f32 v2, v2, s0, v1
	v_med3_f32 v3, v3, s0, v1
	v_mov_b32_e32 v26, v5
	v_cvt_pk_fp8_f32 v26, v2, v3
	v_mul_f32_e32 v4, 0x43800000, v32
	v_mul_f32_e32 v2, 0x43800000, v24
	v_med3_f32 v3, v4, s0, v1
	v_med3_f32 v2, v2, s0, v1
	v_cvt_pk_fp8_f32 v26, v3, v2 op_sel:[0,0,1]
	v_mul_f32_e32 v2, 0x43800000, v40
	v_mul_f32_e32 v3, 0x43800000, v52
	v_med3_f32 v2, v2, s0, v1
	v_med3_f32 v3, v3, s0, v1
	v_mov_b32_e32 v27, v5
	v_cvt_pk_fp8_f32 v27, v2, v3
	v_mul_f32_e32 v4, 0x43800000, v72
	v_mul_f32_e32 v2, 0x43800000, v60
	v_med3_f32 v3, v4, s0, v1
	v_med3_f32 v2, v2, s0, v1
	v_cvt_pk_fp8_f32 v27, v3, v2 op_sel:[0,0,1]
	v_mul_f32_e32 v2, 0x43800000, v76
	v_mul_f32_e32 v3, 0x43800000, v84
	v_med3_f32 v2, v2, s0, v1
	v_med3_f32 v3, v3, s0, v1
	v_mov_b32_e32 v28, v5
	v_cvt_pk_fp8_f32 v28, v2, v3
	v_mul_f32_e32 v4, 0x43800000, v104
	v_mul_f32_e32 v2, 0x43800000, v92
	v_med3_f32 v3, v4, s0, v1
	v_med3_f32 v2, v2, s0, v1
	v_cvt_pk_fp8_f32 v28, v3, v2 op_sel:[0,0,1]
	v_mul_f32_e32 v2, 0x43800000, v108
	v_mul_f32_e32 v3, 0x43800000, v116
	v_med3_f32 v2, v2, s0, v1
	v_med3_f32 v3, v3, s0, v1
	v_mov_b32_e32 v29, v5
	v_cvt_pk_fp8_f32 v29, v2, v3
	v_mul_f32_e32 v4, 0x43800000, v132
	v_mul_f32_e32 v2, 0x43800000, v124
	v_med3_f32 v3, v4, s0, v1
	v_med3_f32 v2, v2, s0, v1
	v_cvt_pk_fp8_f32 v29, v3, v2 op_sel:[0,0,1]
	v_mul_f32_e32 v2, 0x43800000, v9
	v_mul_f32_e32 v3, 0x43800000, v17
	v_med3_f32 v6, v2, s0, v1
	v_med3_f32 v3, v3, s0, v1
	v_mov_b32_e32 v2, v5
	v_cvt_pk_fp8_f32 v2, v6, v3
	v_mul_f32_e32 v4, 0x43800000, v33
	v_mul_f32_e32 v3, 0x43800000, v25
	v_med3_f32 v4, v4, s0, v1
	v_med3_f32 v3, v3, s0, v1
	v_cvt_pk_fp8_f32 v2, v4, v3 op_sel:[0,0,1]
	v_mul_f32_e32 v3, 0x43800000, v41
	v_mul_f32_e32 v4, 0x43800000, v53
	v_med3_f32 v7, v3, s0, v1
	v_med3_f32 v4, v4, s0, v1
	v_mov_b32_e32 v3, v5
	v_cvt_pk_fp8_f32 v3, v7, v4
	v_mul_f32_e32 v6, 0x43800000, v73
	v_mul_f32_e32 v4, 0x43800000, v61
	v_med3_f32 v6, v6, s0, v1
	v_med3_f32 v4, v4, s0, v1
	v_cvt_pk_fp8_f32 v3, v6, v4 op_sel:[0,0,1]
	v_mul_f32_e32 v4, 0x43800000, v77
	v_mul_f32_e32 v6, 0x43800000, v85
	v_med3_f32 v8, v4, s0, v1
	v_med3_f32 v6, v6, s0, v1
	v_mov_b32_e32 v4, v5
	v_cvt_pk_fp8_f32 v4, v8, v6
	v_mul_f32_e32 v7, 0x43800000, v105
	v_mul_f32_e32 v6, 0x43800000, v93
	v_med3_f32 v7, v7, s0, v1
	v_med3_f32 v6, v6, s0, v1
	v_cvt_pk_fp8_f32 v4, v7, v6 op_sel:[0,0,1]
	v_mul_f32_e32 v6, 0x43800000, v109
	v_mul_f32_e32 v7, 0x43800000, v117
	v_med3_f32 v6, v6, s0, v1
	v_med3_f32 v7, v7, s0, v1
	v_cvt_pk_fp8_f32 v5, v6, v7
	v_mul_f32_e32 v8, 0x43800000, v133
	v_mul_f32_e32 v6, 0x43800000, v125
	v_med3_f32 v7, v8, s0, v1
	v_med3_f32 v1, v6, s0, v1
	v_cvt_pk_fp8_f32 v5, v7, v1 op_sel:[0,0,1]
	ds_write_b128 v166, v[10:13] offset:34816
	ds_write_b128 v166, v[18:21] offset:35088
	ds_write_b128 v166, v[26:29] offset:35360
	ds_write_b128 v166, v[2:5] offset:35632
	s_waitcnt lgkmcnt(0)
	s_barrier
	ds_read_b128 v[2:5], v154 offset:34816
	ds_read_b128 v[6:9], v156 offset:34816
	ds_read_b128 v[10:13], v158 offset:34816
	ds_read_b128 v[14:17], v162 offset:34816
	s_waitcnt lgkmcnt(3)
	global_store_dwordx4 v[150:151], v[2:5], off offset:1792 nt
	s_waitcnt lgkmcnt(2)
	global_store_dwordx4 v[152:153], v[6:9], off offset:1792 nt
	s_waitcnt lgkmcnt(1)
	global_store_dwordx4 v[160:161], v[10:13], off offset:1792 nt
	s_waitcnt lgkmcnt(0)
	global_store_dwordx4 v[164:165], v[14:17], off offset:1792 nt
	s_barrier
	s_mov_b64 s[8:9], 0
.LBB0_276:
	s_andn2_b64 vcc, exec, s[8:9]
	s_cbranch_vccnz .LBB0_278
	s_ashr_i32 s0, s4, 5
	s_ashr_i32 s1, s0, 31
	v_readlane_b32 s8, v254, 4
	s_and_b32 s5, s4, 31
	s_lshl_b64 s[2:3], s[0:1], 25
	v_readlane_b32 s10, v254, 6
	v_readlane_b32 s11, v254, 7
	s_add_u32 s2, s10, s2
	s_addc_u32 s3, s11, s3
	s_lshl_b32 s7, s4, 6
	s_lshl_b32 s4, s4, 11
	s_and_b32 s7, s7, 0x780
	s_and_b32 s4, s4, 0x800
	s_or_b32 s4, s7, s4
	s_lshl_b32 s4, s4, 2
	s_add_u32 s2, s2, s4
	s_addc_u32 s3, s3, 0
	s_lshl_b32 s4, s5, 18
	s_lshl_b64 s[0:1], s[0:1], 23
	s_add_u32 s0, s53, s0
	v_readlane_b32 s5, v255, 5
	v_mov_b32_e32 v134, v0
	s_addc_u32 s1, s5, s1
	v_readlane_b32 s9, v254, 5
	v_readfirstlane_b32 s6, v134
	s_add_u32 s8, s0, s4
	s_addc_u32 s9, s1, 0
	s_ashr_i32 s0, s6, 1
	v_lshrrev_b32_e32 v1, 1, v134
	s_andn2_b32 s0, s0, 31
	v_and_b32_e32 v135, 16, v1
	v_or_b32_e32 v2, s0, v135
	v_ashrrev_i32_e32 v3, 31, v2
	v_lshlrev_b32_e32 v1, 2, v134
	v_lshlrev_b64 v[2:3], 14, v[2:3]
	v_and_b32_e32 v140, 0x7c, v1
	v_lshl_add_u64 v[2:3], s[2:3], 0, v[2:3]
	s_waitcnt lgkmcnt(0)
	v_lshlrev_b32_e32 v4, 2, v140
	v_mov_b32_e32 v5, 0
	v_lshl_add_u64 v[2:3], v[2:3], 0, v[4:5]
	s_movk_i32 s1, 0x4000
	v_add_co_u32_e32 v6, vcc, s1, v2
	s_mov_b32 s1, 0x8000
	s_nop 0
	v_addc_co_u32_e32 v7, vcc, 0, v3, vcc
	global_load_dwordx4 v[34:37], v[2:3], off sc0 nt
	global_load_dwordx4 v[46:49], v[6:7], off sc0 nt
	v_add_co_u32_e32 v6, vcc, s1, v2
	s_mov_b32 s1, 0xc000
	s_nop 0
	v_addc_co_u32_e32 v7, vcc, 0, v3, vcc
	v_add_co_u32_e32 v8, vcc, s1, v2
	s_mov_b32 s1, 0x10000
	s_nop 0
	v_addc_co_u32_e32 v9, vcc, 0, v3, vcc
	global_load_dwordx4 v[62:65], v[6:7], off sc0 nt
	global_load_dwordx4 v[54:57], v[8:9], off sc0 nt
	v_add_co_u32_e32 v6, vcc, s1, v2
	s_mov_b32 s1, 0x14000
	s_nop 0
	v_addc_co_u32_e32 v7, vcc, 0, v3, vcc
	v_add_co_u32_e32 v8, vcc, s1, v2
	s_mov_b32 s1, 0x18000
	s_nop 0
	v_addc_co_u32_e32 v9, vcc, 0, v3, vcc
	global_load_dwordx4 v[66:69], v[6:7], off sc0 nt
	global_load_dwordx4 v[78:81], v[8:9], off sc0 nt
	v_add_co_u32_e32 v6, vcc, s1, v2
	s_mov_b32 s1, 0x1c000
	s_nop 0
	v_addc_co_u32_e32 v7, vcc, 0, v3, vcc
	v_add_co_u32_e32 v8, vcc, s1, v2
	s_mov_b32 s1, 0x20000
	s_nop 0
	v_addc_co_u32_e32 v9, vcc, 0, v3, vcc
	global_load_dwordx4 v[94:97], v[6:7], off sc0 nt
	global_load_dwordx4 v[86:89], v[8:9], off sc0 nt
	v_add_co_u32_e32 v6, vcc, s1, v2
	s_mov_b32 s1, 0x24000
	s_nop 0
	v_addc_co_u32_e32 v7, vcc, 0, v3, vcc
	v_add_co_u32_e32 v8, vcc, s1, v2
	s_mov_b32 s1, 0x28000
	s_nop 0
	v_addc_co_u32_e32 v9, vcc, 0, v3, vcc
	global_load_dwordx4 v[98:101], v[6:7], off sc0 nt
	global_load_dwordx4 v[106:109], v[8:9], off sc0 nt
	v_add_co_u32_e32 v6, vcc, s1, v2
	s_mov_b32 s1, 0x2c000
	s_nop 0
	v_addc_co_u32_e32 v7, vcc, 0, v3, vcc
	v_add_co_u32_e32 v8, vcc, s1, v2
	s_mov_b32 s1, 0x30000
	s_nop 0
	v_addc_co_u32_e32 v9, vcc, 0, v3, vcc
	global_load_dwordx4 v[114:117], v[6:7], off sc0 nt
	global_load_dwordx4 v[110:113], v[8:9], off sc0 nt
	v_add_co_u32_e32 v6, vcc, s1, v2
	s_mov_b32 s1, 0x34000
	s_nop 0
	v_addc_co_u32_e32 v7, vcc, 0, v3, vcc
	v_add_co_u32_e32 v8, vcc, s1, v2
	s_mov_b32 s1, 0x38000
	s_nop 0
	v_addc_co_u32_e32 v9, vcc, 0, v3, vcc
	global_load_dwordx4 v[118:121], v[6:7], off sc0 nt
	global_load_dwordx4 v[122:125], v[8:9], off sc0 nt
	v_add_co_u32_e32 v6, vcc, s1, v2
	s_mov_b32 s1, 0x3c000
	s_nop 0
	v_addc_co_u32_e32 v7, vcc, 0, v3, vcc
	v_add_co_u32_e32 v8, vcc, s1, v2
	s_mov_b32 s1, 0x400000
	s_nop 0
	v_addc_co_u32_e32 v9, vcc, 0, v3, vcc
	global_load_dwordx4 v[130:133], v[6:7], off sc0 nt
	global_load_dwordx4 v[126:129], v[8:9], off sc0 nt
	v_add_co_u32_e32 v6, vcc, s1, v2
	s_mov_b32 s1, 0x404000
	s_nop 0
	v_addc_co_u32_e32 v7, vcc, 0, v3, vcc
	v_add_co_u32_e32 v10, vcc, s1, v2
	s_mov_b32 s1, 0x408000
	s_nop 0
	v_addc_co_u32_e32 v11, vcc, 0, v3, vcc
	v_add_co_u32_e32 v14, vcc, s1, v2
	s_mov_b32 s1, 0x40c000
	s_nop 0
	v_addc_co_u32_e32 v15, vcc, 0, v3, vcc
	v_add_co_u32_e32 v16, vcc, s1, v2
	s_mov_b32 s1, 0x410000
	s_nop 0
	v_addc_co_u32_e32 v17, vcc, 0, v3, vcc
	v_add_co_u32_e32 v22, vcc, s1, v2
	s_mov_b32 s1, 0x414000
	s_nop 0
	v_addc_co_u32_e32 v23, vcc, 0, v3, vcc
	v_add_co_u32_e32 v26, vcc, s1, v2
	s_mov_b32 s1, 0x418000
	s_nop 0
	v_addc_co_u32_e32 v27, vcc, 0, v3, vcc
	v_add_co_u32_e32 v30, vcc, s1, v2
	s_mov_b32 s1, 0x41c000
	s_nop 0
	v_addc_co_u32_e32 v31, vcc, 0, v3, vcc
	v_add_co_u32_e32 v32, vcc, s1, v2
	s_mov_b32 s1, 0x420000
	s_nop 0
	v_addc_co_u32_e32 v33, vcc, 0, v3, vcc
	v_add_co_u32_e32 v42, vcc, s1, v2
	s_mov_b32 s1, 0x424000
	s_nop 0
	v_addc_co_u32_e32 v43, vcc, 0, v3, vcc
	v_add_co_u32_e32 v50, vcc, s1, v2
	s_mov_b32 s1, 0x428000
	s_nop 0
	v_addc_co_u32_e32 v51, vcc, 0, v3, vcc
	v_add_co_u32_e32 v58, vcc, s1, v2
	s_mov_b32 s1, 0x42c000
	s_nop 0
	v_addc_co_u32_e32 v59, vcc, 0, v3, vcc
	v_add_co_u32_e32 v60, vcc, s1, v2
	s_mov_b32 s1, 0x430000
	s_nop 0
	v_addc_co_u32_e32 v61, vcc, 0, v3, vcc
	v_add_co_u32_e32 v74, vcc, s1, v2
	s_mov_b32 s1, 0x434000
	s_nop 0
	v_addc_co_u32_e32 v75, vcc, 0, v3, vcc
	v_add_co_u32_e32 v82, vcc, s1, v2
	s_mov_b32 s1, 0x438000
	s_nop 0
	v_addc_co_u32_e32 v83, vcc, 0, v3, vcc
	v_add_co_u32_e32 v90, vcc, s1, v2
	s_mov_b32 s1, 0x43c000
	s_nop 0
	v_addc_co_u32_e32 v91, vcc, 0, v3, vcc
	v_add_co_u32_e32 v92, vcc, s1, v2
	global_load_dwordx4 v[6:9], v[6:7], off sc0 nt
	s_nop 0
	global_load_dwordx4 v[10:13], v[10:11], off sc0 nt
	v_addc_co_u32_e32 v93, vcc, 0, v3, vcc
	global_load_dwordx4 v[18:21], v[14:15], off sc0 nt
	s_nop 0
	global_load_dwordx4 v[14:17], v[16:17], off sc0 nt
	s_nop 0
	global_load_dwordx4 v[22:25], v[22:23], off sc0 nt
	s_nop 0
	global_load_dwordx4 v[26:29], v[26:27], off sc0 nt
	s_nop 0
	global_load_dwordx4 v[38:41], v[30:31], off sc0 nt
	s_nop 0
	global_load_dwordx4 v[30:33], v[32:33], off sc0 nt
	s_nop 0
	global_load_dwordx4 v[42:45], v[42:43], off sc0 nt
	s_nop 0
	global_load_dwordx4 v[50:53], v[50:51], off sc0 nt
	s_nop 0
	global_load_dwordx4 v[70:73], v[58:59], off sc0 nt
	s_nop 0
	global_load_dwordx4 v[58:61], v[60:61], off sc0 nt
	s_nop 0
	global_load_dwordx4 v[74:77], v[74:75], off sc0 nt
	s_nop 0
	global_load_dwordx4 v[82:85], v[82:83], off sc0 nt
	s_nop 0
	global_load_dwordx4 v[102:105], v[90:91], off sc0 nt
	s_nop 0
	global_load_dwordx4 v[90:93], v[92:93], off sc0 nt
	v_readlane_b32 s12, v254, 8
	v_readlane_b32 s13, v254, 9
	v_readlane_b32 s14, v254, 10
	v_readlane_b32 s15, v254, 11
	s_add_i32 s2, s0, 0
	s_waitcnt vmcnt(0)
	v_mul_f32_e32 v4, 0x43800000, v34
	v_mul_f32_e32 v34, 0x43800000, v46
	s_mov_b32 s0, 0xc3e00000
	v_mov_b32_e32 v1, 0x43e00000
	v_med3_f32 v4, v4, s0, v1
	v_med3_f32 v34, v34, s0, v1
	v_mov_b32_e32 v136, v5
	v_cvt_pk_fp8_f32 v136, v4, v34
	v_mul_f32_e32 v46, 0x43800000, v62
	v_mul_f32_e32 v4, 0x43800000, v54
	v_med3_f32 v34, v46, s0, v1
	v_med3_f32 v4, v4, s0, v1
	v_cvt_pk_fp8_f32 v136, v34, v4 op_sel:[0,0,1]
	v_mul_f32_e32 v4, 0x43800000, v66
	v_mul_f32_e32 v34, 0x43800000, v78
	v_med3_f32 v4, v4, s0, v1
	v_med3_f32 v34, v34, s0, v1
	v_mov_b32_e32 v137, v5
	v_cvt_pk_fp8_f32 v137, v4, v34
	v_mul_f32_e32 v46, 0x43800000, v94
	v_mul_f32_e32 v4, 0x43800000, v86
	v_med3_f32 v34, v46, s0, v1
	v_med3_f32 v4, v4, s0, v1
	v_cvt_pk_fp8_f32 v137, v34, v4 op_sel:[0,0,1]
	v_mul_f32_e32 v4, 0x43800000, v98
	v_mul_f32_e32 v34, 0x43800000, v106
	v_med3_f32 v4, v4, s0, v1
	v_med3_f32 v34, v34, s0, v1
	v_mov_b32_e32 v138, v5
	v_cvt_pk_fp8_f32 v138, v4, v34
	v_mul_f32_e32 v46, 0x43800000, v114
	v_mul_f32_e32 v4, 0x43800000, v110
	v_med3_f32 v34, v46, s0, v1
	v_med3_f32 v4, v4, s0, v1
	v_cvt_pk_fp8_f32 v138, v34, v4 op_sel:[0,0,1]
	v_mul_f32_e32 v4, 0x43800000, v118
	v_mul_f32_e32 v34, 0x43800000, v122
	v_med3_f32 v4, v4, s0, v1
	v_med3_f32 v34, v34, s0, v1
	v_mov_b32_e32 v139, v5
	v_cvt_pk_fp8_f32 v139, v4, v34
	v_mul_f32_e32 v46, 0x43800000, v130
	v_mul_f32_e32 v4, 0x43800000, v126
	v_med3_f32 v34, v46, s0, v1
	v_med3_f32 v4, v4, s0, v1
	v_cvt_pk_fp8_f32 v139, v34, v4 op_sel:[0,0,1]
	v_mul_u32_u24_e32 v4, 0x110, v140
	v_add3_u32 v166, s2, v135, v4
	v_mul_f32_e32 v4, 0x43800000, v35
	v_mul_f32_e32 v34, 0x43800000, v47
	v_med3_f32 v4, v4, s0, v1
	v_med3_f32 v34, v34, s0, v1
	v_mov_b32_e32 v140, v5
	v_cvt_pk_fp8_f32 v140, v4, v34
	v_mul_f32_e32 v35, 0x43800000, v63
	v_mul_f32_e32 v4, 0x43800000, v55
	v_med3_f32 v34, v35, s0, v1
	v_med3_f32 v4, v4, s0, v1
	v_cvt_pk_fp8_f32 v140, v34, v4 op_sel:[0,0,1]
	v_mul_f32_e32 v4, 0x43800000, v67
	v_mul_f32_e32 v34, 0x43800000, v79
	v_med3_f32 v4, v4, s0, v1
	v_med3_f32 v34, v34, s0, v1
	v_mov_b32_e32 v141, v5
	v_cvt_pk_fp8_f32 v141, v4, v34
	v_mul_f32_e32 v35, 0x43800000, v95
	v_mul_f32_e32 v4, 0x43800000, v87
	v_med3_f32 v34, v35, s0, v1
	v_med3_f32 v4, v4, s0, v1
	v_cvt_pk_fp8_f32 v141, v34, v4 op_sel:[0,0,1]
	v_mul_f32_e32 v4, 0x43800000, v99
	v_mul_f32_e32 v34, 0x43800000, v107
	v_med3_f32 v4, v4, s0, v1
	v_med3_f32 v34, v34, s0, v1
	v_mov_b32_e32 v142, v5
	v_cvt_pk_fp8_f32 v142, v4, v34
	v_mul_f32_e32 v35, 0x43800000, v115
	v_mul_f32_e32 v4, 0x43800000, v111
	v_med3_f32 v34, v35, s0, v1
	v_med3_f32 v4, v4, s0, v1
	v_cvt_pk_fp8_f32 v142, v34, v4 op_sel:[0,0,1]
	v_mul_f32_e32 v4, 0x43800000, v119
	v_mul_f32_e32 v34, 0x43800000, v123
	v_med3_f32 v4, v4, s0, v1
	v_med3_f32 v34, v34, s0, v1
	v_mov_b32_e32 v143, v5
	v_cvt_pk_fp8_f32 v143, v4, v34
	v_mul_f32_e32 v35, 0x43800000, v131
	v_mul_f32_e32 v4, 0x43800000, v127
	v_med3_f32 v34, v35, s0, v1
	v_med3_f32 v4, v4, s0, v1
	v_cvt_pk_fp8_f32 v143, v34, v4 op_sel:[0,0,1]
	v_mul_f32_e32 v4, 0x43800000, v36
	v_mul_f32_e32 v34, 0x43800000, v48
	v_med3_f32 v4, v4, s0, v1
	v_med3_f32 v34, v34, s0, v1
	v_mov_b32_e32 v144, v5
	v_cvt_pk_fp8_f32 v144, v4, v34
	v_mul_f32_e32 v35, 0x43800000, v64
	v_mul_f32_e32 v4, 0x43800000, v56
	v_med3_f32 v34, v35, s0, v1
	v_med3_f32 v4, v4, s0, v1
	v_cvt_pk_fp8_f32 v144, v34, v4 op_sel:[0,0,1]
	v_mul_f32_e32 v4, 0x43800000, v68
	v_mul_f32_e32 v34, 0x43800000, v80
	v_med3_f32 v4, v4, s0, v1
	v_med3_f32 v34, v34, s0, v1
	v_mov_b32_e32 v145, v5
	v_cvt_pk_fp8_f32 v145, v4, v34
	v_mul_f32_e32 v35, 0x43800000, v96
	v_mul_f32_e32 v4, 0x43800000, v88
	v_med3_f32 v34, v35, s0, v1
	v_med3_f32 v4, v4, s0, v1
	v_cvt_pk_fp8_f32 v145, v34, v4 op_sel:[0,0,1]
	v_mul_f32_e32 v4, 0x43800000, v100
	v_mul_f32_e32 v34, 0x43800000, v108
	v_med3_f32 v4, v4, s0, v1
	v_med3_f32 v34, v34, s0, v1
	v_mov_b32_e32 v146, v5
	v_cvt_pk_fp8_f32 v146, v4, v34
	v_mul_f32_e32 v35, 0x43800000, v116
	v_mul_f32_e32 v4, 0x43800000, v112
	v_med3_f32 v34, v35, s0, v1
	v_med3_f32 v4, v4, s0, v1
	v_cvt_pk_fp8_f32 v146, v34, v4 op_sel:[0,0,1]
	v_mul_f32_e32 v4, 0x43800000, v120
	v_mul_f32_e32 v34, 0x43800000, v124
	v_med3_f32 v4, v4, s0, v1
	v_med3_f32 v34, v34, s0, v1
	v_mov_b32_e32 v147, v5
	v_cvt_pk_fp8_f32 v147, v4, v34
	v_mul_f32_e32 v35, 0x43800000, v132
	v_mul_f32_e32 v4, 0x43800000, v128
	v_med3_f32 v34, v35, s0, v1
	v_med3_f32 v4, v4, s0, v1
	v_cvt_pk_fp8_f32 v147, v34, v4 op_sel:[0,0,1]
	v_mul_f32_e32 v4, 0x43800000, v37
	v_mul_f32_e32 v34, 0x43800000, v49
	v_med3_f32 v4, v4, s0, v1
	v_med3_f32 v36, v34, s0, v1
	v_mov_b32_e32 v34, v5
	v_cvt_pk_fp8_f32 v34, v4, v36
	v_mul_f32_e32 v35, 0x43800000, v65
	v_mul_f32_e32 v4, 0x43800000, v57
	v_med3_f32 v35, v35, s0, v1
	v_med3_f32 v4, v4, s0, v1
	v_cvt_pk_fp8_f32 v34, v35, v4 op_sel:[0,0,1]
	v_mul_f32_e32 v4, 0x43800000, v69
	v_mul_f32_e32 v35, 0x43800000, v81
	v_med3_f32 v4, v4, s0, v1
	v_med3_f32 v37, v35, s0, v1
	v_mov_b32_e32 v35, v5
	v_cvt_pk_fp8_f32 v35, v4, v37
	v_mul_f32_e32 v36, 0x43800000, v97
	v_mul_f32_e32 v4, 0x43800000, v89
	v_med3_f32 v36, v36, s0, v1
	v_med3_f32 v4, v4, s0, v1
	v_cvt_pk_fp8_f32 v35, v36, v4 op_sel:[0,0,1]
	v_mul_f32_e32 v4, 0x43800000, v101
	v_mul_f32_e32 v36, 0x43800000, v109
	v_med3_f32 v4, v4, s0, v1
	v_med3_f32 v46, v36, s0, v1
	v_mov_b32_e32 v36, v5
	v_cvt_pk_fp8_f32 v36, v4, v46
	v_mul_f32_e32 v37, 0x43800000, v117
	v_mul_f32_e32 v4, 0x43800000, v113
	v_med3_f32 v37, v37, s0, v1
	v_med3_f32 v4, v4, s0, v1
	v_cvt_pk_fp8_f32 v36, v37, v4 op_sel:[0,0,1]
	v_mul_f32_e32 v4, 0x43800000, v121
	v_mul_f32_e32 v37, 0x43800000, v125
	v_med3_f32 v4, v4, s0, v1
	v_med3_f32 v47, v37, s0, v1
	v_mov_b32_e32 v37, v5
	v_cvt_pk_fp8_f32 v37, v4, v47
	v_mul_f32_e32 v46, 0x43800000, v133
	v_mul_f32_e32 v4, 0x43800000, v129
	v_med3_f32 v46, v46, s0, v1
	v_med3_f32 v4, v4, s0, v1
	v_cvt_pk_fp8_f32 v37, v46, v4 op_sel:[0,0,1]
	ds_write_b128 v166, v[136:139]
	ds_write_b128 v166, v[140:143] offset:272
	ds_write_b128 v166, v[144:147] offset:544
	ds_write_b128 v166, v[34:37] offset:816
	v_add_u32_e32 v34, 0x200, v134
	v_ashrrev_i32_e32 v140, 4, v34
	v_add_u32_e32 v34, 0x400, v134
	v_ashrrev_i32_e32 v144, 4, v34
	v_add_u32_e32 v34, 0x600, v134
	v_ashrrev_i32_e32 v136, 4, v134
	v_ashrrev_i32_e32 v148, 4, v34
	v_lshlrev_b32_e32 v4, 4, v134
	v_ashrrev_i32_e32 v137, 31, v136
	v_ashrrev_i32_e32 v141, 31, v140
	v_ashrrev_i32_e32 v145, 31, v144
	v_ashrrev_i32_e32 v149, 31, v148
	s_movk_i32 s1, 0x110
	s_waitcnt lgkmcnt(0)
	s_barrier
	v_and_b32_e32 v4, 0xf0, v4
	v_lshlrev_b64 v[138:139], 11, v[136:137]
	v_lshlrev_b64 v[142:143], 11, v[140:141]
	v_lshlrev_b64 v[146:147], 11, v[144:145]
	v_lshlrev_b64 v[164:165], 11, v[148:149]
	s_mov_b32 s2, 0x800000
	v_add_co_u32_e32 v34, vcc, s2, v2
	s_mov_b32 s2, 0x804000
	s_nop 0
	v_addc_co_u32_e32 v35, vcc, 0, v3, vcc
	v_add_co_u32_e32 v46, vcc, s2, v2
	s_mov_b32 s2, 0x808000
	s_nop 0
	v_addc_co_u32_e32 v47, vcc, 0, v3, vcc
	v_add_co_u32_e32 v54, vcc, s2, v2
	s_mov_b32 s2, 0x80c000
	s_nop 0
	v_addc_co_u32_e32 v55, vcc, 0, v3, vcc
	v_add_co_u32_e32 v56, vcc, s2, v2
	s_mov_b32 s2, 0x810000
	s_nop 0
	v_addc_co_u32_e32 v57, vcc, 0, v3, vcc
	v_add_co_u32_e32 v66, vcc, s2, v2
	s_mov_b32 s2, 0x814000
	s_nop 0
	v_addc_co_u32_e32 v67, vcc, 0, v3, vcc
	v_add_co_u32_e32 v78, vcc, s2, v2
	s_mov_b32 s2, 0x818000
	s_nop 0
	v_addc_co_u32_e32 v79, vcc, 0, v3, vcc
	v_add_co_u32_e32 v86, vcc, s2, v2
	s_mov_b32 s2, 0x81c000
	s_nop 0
	v_addc_co_u32_e32 v87, vcc, 0, v3, vcc
	v_add_co_u32_e32 v88, vcc, s2, v2
	s_mov_b32 s2, 0x820000
	s_nop 0
	v_addc_co_u32_e32 v89, vcc, 0, v3, vcc
	v_add_co_u32_e32 v98, vcc, s2, v2
	s_mov_b32 s2, 0x824000
	s_nop 0
	v_addc_co_u32_e32 v99, vcc, 0, v3, vcc
	v_add_co_u32_e32 v106, vcc, s2, v2
	s_mov_b32 s2, 0x828000
	s_nop 0
	v_addc_co_u32_e32 v107, vcc, 0, v3, vcc
	v_add_co_u32_e32 v110, vcc, s2, v2
	s_mov_b32 s2, 0x82c000
	s_nop 0
	v_addc_co_u32_e32 v111, vcc, 0, v3, vcc
	v_add_co_u32_e32 v112, vcc, s2, v2
	s_mov_b32 s2, 0x830000
	s_nop 0
	v_addc_co_u32_e32 v113, vcc, 0, v3, vcc
	v_add_co_u32_e32 v118, vcc, s2, v2
	s_mov_b32 s2, 0x834000
	s_nop 0
	v_addc_co_u32_e32 v119, vcc, 0, v3, vcc
	v_add_co_u32_e32 v122, vcc, s2, v2
	s_mov_b32 s2, 0x838000
	s_nop 0
	v_addc_co_u32_e32 v123, vcc, 0, v3, vcc
	v_add_co_u32_e32 v126, vcc, s2, v2
	s_mov_b32 s2, 0x83c000
	s_nop 0
	v_addc_co_u32_e32 v127, vcc, 0, v3, vcc
	v_add_co_u32_e32 v128, vcc, s2, v2
	global_load_dwordx4 v[34:37], v[34:35], off sc0 nt
	s_nop 0
	global_load_dwordx4 v[46:49], v[46:47], off sc0 nt
	v_addc_co_u32_e32 v129, vcc, 0, v3, vcc
	global_load_dwordx4 v[62:65], v[54:55], off sc0 nt
	s_nop 0
	global_load_dwordx4 v[54:57], v[56:57], off sc0 nt
	s_nop 0
	global_load_dwordx4 v[66:69], v[66:67], off sc0 nt
	s_nop 0
	global_load_dwordx4 v[78:81], v[78:79], off sc0 nt
	s_nop 0
	global_load_dwordx4 v[94:97], v[86:87], off sc0 nt
	s_nop 0
	global_load_dwordx4 v[86:89], v[88:89], off sc0 nt
	s_nop 0
	global_load_dwordx4 v[98:101], v[98:99], off sc0 nt
	s_nop 0
	global_load_dwordx4 v[106:109], v[106:107], off sc0 nt
	s_nop 0
	global_load_dwordx4 v[114:117], v[110:111], off sc0 nt
	s_nop 0
	global_load_dwordx4 v[110:113], v[112:113], off sc0 nt
	s_nop 0
	global_load_dwordx4 v[118:121], v[118:119], off sc0 nt
	s_nop 0
	global_load_dwordx4 v[122:125], v[122:123], off sc0 nt
	s_nop 0
	global_load_dwordx4 v[130:133], v[126:127], off sc0 nt
	s_nop 0
	global_load_dwordx4 v[126:129], v[128:129], off sc0 nt
	v_add_u32_e32 v160, 0, v4
	v_mad_u64_u32 v[154:155], s[2:3], v136, s1, v[160:161]
	ds_read_b128 v[134:137], v154
	v_lshl_add_u64 v[168:169], s[8:9], 0, v[4:5]
	v_lshl_add_u64 v[150:151], v[168:169], 0, v[138:139]
	v_mad_u64_u32 v[156:157], s[2:3], v140, s1, v[160:161]
	v_mad_u64_u32 v[158:159], s[2:3], v144, s1, v[160:161]
	v_mad_u64_u32 v[162:163], s[2:3], v148, s1, v[160:161]
	ds_read_b128 v[138:141], v156
	s_waitcnt lgkmcnt(1)
	global_store_dwordx4 v[150:151], v[134:137], off nt
	v_lshl_add_u64 v[152:153], v[168:169], 0, v[142:143]
	ds_read_b128 v[134:137], v158
	ds_read_b128 v[142:145], v162
	v_lshl_add_u64 v[160:161], v[168:169], 0, v[146:147]
	v_lshl_add_u64 v[164:165], v[168:169], 0, v[164:165]
	s_waitcnt lgkmcnt(2)
	global_store_dwordx4 v[152:153], v[138:141], off nt
	s_waitcnt lgkmcnt(1)
	global_store_dwordx4 v[160:161], v[134:137], off nt
	s_waitcnt lgkmcnt(0)
	global_store_dwordx4 v[164:165], v[142:145], off nt
	v_mul_f32_e32 v4, 0x43800000, v6
	v_mul_f32_e32 v6, 0x43800000, v10
	v_med3_f32 v4, v4, s0, v1
	v_med3_f32 v6, v6, s0, v1
	v_mov_b32_e32 v134, v5
	v_cvt_pk_fp8_f32 v134, v4, v6
	v_mul_f32_e32 v10, 0x43800000, v18
	v_mul_f32_e32 v4, 0x43800000, v14
	v_med3_f32 v6, v10, s0, v1
	v_med3_f32 v4, v4, s0, v1
	v_cvt_pk_fp8_f32 v134, v6, v4 op_sel:[0,0,1]
	v_mul_f32_e32 v4, 0x43800000, v22
	v_mul_f32_e32 v6, 0x43800000, v26
	v_med3_f32 v4, v4, s0, v1
	v_med3_f32 v6, v6, s0, v1
	v_mov_b32_e32 v135, v5
	v_cvt_pk_fp8_f32 v135, v4, v6
	v_mul_f32_e32 v10, 0x43800000, v38
	v_mul_f32_e32 v4, 0x43800000, v30
	v_med3_f32 v6, v10, s0, v1
	v_med3_f32 v4, v4, s0, v1
	v_cvt_pk_fp8_f32 v135, v6, v4 op_sel:[0,0,1]
	v_mul_f32_e32 v4, 0x43800000, v42
	v_mul_f32_e32 v6, 0x43800000, v50
	v_med3_f32 v4, v4, s0, v1
	v_med3_f32 v6, v6, s0, v1
	v_mov_b32_e32 v136, v5
	v_cvt_pk_fp8_f32 v136, v4, v6
	v_mul_f32_e32 v10, 0x43800000, v70
	v_mul_f32_e32 v4, 0x43800000, v58
	v_med3_f32 v6, v10, s0, v1
	v_med3_f32 v4, v4, s0, v1
	v_cvt_pk_fp8_f32 v136, v6, v4 op_sel:[0,0,1]
	v_mul_f32_e32 v4, 0x43800000, v74
	v_mul_f32_e32 v6, 0x43800000, v82
	v_med3_f32 v4, v4, s0, v1
	v_med3_f32 v6, v6, s0, v1
	v_mov_b32_e32 v137, v5
	v_cvt_pk_fp8_f32 v137, v4, v6
	v_mul_f32_e32 v10, 0x43800000, v102
	v_mul_f32_e32 v4, 0x43800000, v90
	v_med3_f32 v6, v10, s0, v1
	v_med3_f32 v4, v4, s0, v1
	v_cvt_pk_fp8_f32 v137, v6, v4 op_sel:[0,0,1]
	v_mul_f32_e32 v4, 0x43800000, v7
	v_mul_f32_e32 v6, 0x43800000, v11
	v_med3_f32 v4, v4, s0, v1
	v_med3_f32 v6, v6, s0, v1
	v_mov_b32_e32 v138, v5
	v_cvt_pk_fp8_f32 v138, v4, v6
	v_mul_f32_e32 v7, 0x43800000, v19
	v_mul_f32_e32 v4, 0x43800000, v15
	v_med3_f32 v6, v7, s0, v1
	v_med3_f32 v4, v4, s0, v1
	v_cvt_pk_fp8_f32 v138, v6, v4 op_sel:[0,0,1]
	v_mul_f32_e32 v4, 0x43800000, v23
	v_mul_f32_e32 v6, 0x43800000, v27
	v_med3_f32 v4, v4, s0, v1
	v_med3_f32 v6, v6, s0, v1
	v_mov_b32_e32 v139, v5
	v_cvt_pk_fp8_f32 v139, v4, v6
	v_mul_f32_e32 v7, 0x43800000, v39
	v_mul_f32_e32 v4, 0x43800000, v31
	v_med3_f32 v6, v7, s0, v1
	v_med3_f32 v4, v4, s0, v1
	v_cvt_pk_fp8_f32 v139, v6, v4 op_sel:[0,0,1]
	v_mul_f32_e32 v4, 0x43800000, v43
	v_mul_f32_e32 v6, 0x43800000, v51
	v_med3_f32 v4, v4, s0, v1
	v_med3_f32 v6, v6, s0, v1
	v_mov_b32_e32 v140, v5
	v_cvt_pk_fp8_f32 v140, v4, v6
	v_mul_f32_e32 v7, 0x43800000, v71
	v_mul_f32_e32 v4, 0x43800000, v59
	v_med3_f32 v6, v7, s0, v1
	v_med3_f32 v4, v4, s0, v1
	v_cvt_pk_fp8_f32 v140, v6, v4 op_sel:[0,0,1]
	v_mul_f32_e32 v4, 0x43800000, v75
	v_mul_f32_e32 v6, 0x43800000, v83
	v_med3_f32 v4, v4, s0, v1
	v_med3_f32 v6, v6, s0, v1
	v_mov_b32_e32 v141, v5
	v_cvt_pk_fp8_f32 v141, v4, v6
	v_mul_f32_e32 v7, 0x43800000, v103
	v_mul_f32_e32 v4, 0x43800000, v91
	v_med3_f32 v6, v7, s0, v1
	v_med3_f32 v4, v4, s0, v1
	v_cvt_pk_fp8_f32 v141, v6, v4 op_sel:[0,0,1]
	v_mul_f32_e32 v4, 0x43800000, v8
	v_mul_f32_e32 v6, 0x43800000, v12
	v_med3_f32 v4, v4, s0, v1
	v_med3_f32 v6, v6, s0, v1
	v_mov_b32_e32 v142, v5
	v_cvt_pk_fp8_f32 v142, v4, v6
	v_mul_f32_e32 v7, 0x43800000, v20
	v_mul_f32_e32 v4, 0x43800000, v16
	v_med3_f32 v6, v7, s0, v1
	v_med3_f32 v4, v4, s0, v1
	v_cvt_pk_fp8_f32 v142, v6, v4 op_sel:[0,0,1]
	v_mul_f32_e32 v4, 0x43800000, v24
	v_mul_f32_e32 v6, 0x43800000, v28
	v_med3_f32 v4, v4, s0, v1
	v_med3_f32 v6, v6, s0, v1
	v_mov_b32_e32 v143, v5
	v_cvt_pk_fp8_f32 v143, v4, v6
	v_mul_f32_e32 v7, 0x43800000, v40
	v_mul_f32_e32 v4, 0x43800000, v32
	v_med3_f32 v6, v7, s0, v1
	v_med3_f32 v4, v4, s0, v1
	v_cvt_pk_fp8_f32 v143, v6, v4 op_sel:[0,0,1]
	v_mul_f32_e32 v4, 0x43800000, v44
	v_mul_f32_e32 v6, 0x43800000, v52
	v_med3_f32 v4, v4, s0, v1
	v_med3_f32 v6, v6, s0, v1
	v_mov_b32_e32 v144, v5
	v_cvt_pk_fp8_f32 v144, v4, v6
	v_mul_f32_e32 v7, 0x43800000, v72
	v_mul_f32_e32 v4, 0x43800000, v60
	v_med3_f32 v6, v7, s0, v1
	v_med3_f32 v4, v4, s0, v1
	v_cvt_pk_fp8_f32 v144, v6, v4 op_sel:[0,0,1]
	v_mul_f32_e32 v4, 0x43800000, v76
	v_mul_f32_e32 v6, 0x43800000, v84
	v_med3_f32 v4, v4, s0, v1
	v_med3_f32 v6, v6, s0, v1
	v_mov_b32_e32 v145, v5
	v_cvt_pk_fp8_f32 v145, v4, v6
	v_mul_f32_e32 v7, 0x43800000, v104
	v_mul_f32_e32 v4, 0x43800000, v92
	v_med3_f32 v6, v7, s0, v1
	v_med3_f32 v4, v4, s0, v1
	v_cvt_pk_fp8_f32 v145, v6, v4 op_sel:[0,0,1]
	v_mul_f32_e32 v4, 0x43800000, v9
	v_mul_f32_e32 v6, 0x43800000, v13
	v_med3_f32 v4, v4, s0, v1
	v_med3_f32 v8, v6, s0, v1
	v_mov_b32_e32 v6, v5
	v_cvt_pk_fp8_f32 v6, v4, v8
	v_mul_f32_e32 v7, 0x43800000, v21
	v_mul_f32_e32 v4, 0x43800000, v17
	v_med3_f32 v7, v7, s0, v1
	v_med3_f32 v4, v4, s0, v1
	v_cvt_pk_fp8_f32 v6, v7, v4 op_sel:[0,0,1]
	v_mul_f32_e32 v4, 0x43800000, v25
	v_mul_f32_e32 v7, 0x43800000, v29
	v_med3_f32 v4, v4, s0, v1
	v_med3_f32 v9, v7, s0, v1
	v_mov_b32_e32 v7, v5
	v_cvt_pk_fp8_f32 v7, v4, v9
	v_mul_f32_e32 v8, 0x43800000, v41
	v_mul_f32_e32 v4, 0x43800000, v33
	v_med3_f32 v8, v8, s0, v1
	v_med3_f32 v4, v4, s0, v1
	v_cvt_pk_fp8_f32 v7, v8, v4 op_sel:[0,0,1]
	v_mul_f32_e32 v4, 0x43800000, v45
	v_mul_f32_e32 v8, 0x43800000, v53
	v_med3_f32 v4, v4, s0, v1
	v_med3_f32 v10, v8, s0, v1
	v_mov_b32_e32 v8, v5
	v_cvt_pk_fp8_f32 v8, v4, v10
	v_mul_f32_e32 v9, 0x43800000, v73
	v_mul_f32_e32 v4, 0x43800000, v61
	v_med3_f32 v9, v9, s0, v1
	v_med3_f32 v4, v4, s0, v1
	v_cvt_pk_fp8_f32 v8, v9, v4 op_sel:[0,0,1]
	v_mul_f32_e32 v4, 0x43800000, v77
	v_mul_f32_e32 v9, 0x43800000, v85
	v_med3_f32 v4, v4, s0, v1
	v_med3_f32 v11, v9, s0, v1
	v_mov_b32_e32 v9, v5
	v_cvt_pk_fp8_f32 v9, v4, v11
	v_mul_f32_e32 v10, 0x43800000, v105
	v_mul_f32_e32 v4, 0x43800000, v93
	v_med3_f32 v10, v10, s0, v1
	v_med3_f32 v4, v4, s0, v1
	v_cvt_pk_fp8_f32 v9, v10, v4 op_sel:[0,0,1]
	ds_write_b128 v166, v[134:137] offset:34816
	ds_write_b128 v166, v[138:141] offset:35088
	ds_write_b128 v166, v[142:145] offset:35360
	ds_write_b128 v166, v[6:9] offset:35632
	s_waitcnt lgkmcnt(0)
	s_barrier
	s_mov_b32 s1, 0xc00000
	v_add_co_u32_e32 v6, vcc, s1, v2
	s_mov_b32 s1, 0xc04000
	s_nop 0
	v_addc_co_u32_e32 v7, vcc, 0, v3, vcc
	v_add_co_u32_e32 v10, vcc, s1, v2
	s_mov_b32 s1, 0xc08000
	s_nop 0
	v_addc_co_u32_e32 v11, vcc, 0, v3, vcc
	global_load_dwordx4 v[6:9], v[6:7], off sc0 nt
	s_nop 0
	global_load_dwordx4 v[14:17], v[10:11], off sc0 nt
	v_add_co_u32_e32 v10, vcc, s1, v2
	s_mov_b32 s1, 0xc0c000
	s_nop 0
	v_addc_co_u32_e32 v11, vcc, 0, v3, vcc
	v_add_co_u32_e32 v12, vcc, s1, v2
	s_mov_b32 s1, 0xc10000
	s_nop 0
	v_addc_co_u32_e32 v13, vcc, 0, v3, vcc
	global_load_dwordx4 v[30:33], v[10:11], off sc0 nt
	global_load_dwordx4 v[22:25], v[12:13], off sc0 nt
	v_add_co_u32_e32 v10, vcc, s1, v2
	s_mov_b32 s1, 0xc14000
	s_nop 0
	v_addc_co_u32_e32 v11, vcc, 0, v3, vcc
	v_add_co_u32_e32 v12, vcc, s1, v2
	s_mov_b32 s1, 0xc18000
	s_nop 0
	v_addc_co_u32_e32 v13, vcc, 0, v3, vcc
	global_load_dwordx4 v[38:41], v[10:11], off sc0 nt
	global_load_dwordx4 v[50:53], v[12:13], off sc0 nt
	v_add_co_u32_e32 v10, vcc, s1, v2
	s_mov_b32 s1, 0xc1c000
	s_nop 0
	v_addc_co_u32_e32 v11, vcc, 0, v3, vcc
	v_add_co_u32_e32 v12, vcc, s1, v2
	s_mov_b32 s1, 0xc20000
	s_nop 0
	v_addc_co_u32_e32 v13, vcc, 0, v3, vcc
	global_load_dwordx4 v[70:73], v[10:11], off sc0 nt
	global_load_dwordx4 v[58:61], v[12:13], off sc0 nt
	v_add_co_u32_e32 v10, vcc, s1, v2
	s_mov_b32 s1, 0xc24000
	s_nop 0
	v_addc_co_u32_e32 v11, vcc, 0, v3, vcc
	v_add_co_u32_e32 v12, vcc, s1, v2
	s_mov_b32 s1, 0xc28000
	s_nop 0
	v_addc_co_u32_e32 v13, vcc, 0, v3, vcc
	global_load_dwordx4 v[74:77], v[10:11], off sc0 nt
	global_load_dwordx4 v[82:85], v[12:13], off sc0 nt
	v_add_co_u32_e32 v10, vcc, s1, v2
	s_mov_b32 s1, 0xc2c000
	s_nop 0
	v_addc_co_u32_e32 v11, vcc, 0, v3, vcc
	v_add_co_u32_e32 v12, vcc, s1, v2
	s_mov_b32 s1, 0xc30000
	s_nop 0
	v_addc_co_u32_e32 v13, vcc, 0, v3, vcc
	global_load_dwordx4 v[102:105], v[10:11], off sc0 nt
	global_load_dwordx4 v[90:93], v[12:13], off sc0 nt
	v_add_co_u32_e32 v10, vcc, s1, v2
	s_mov_b32 s1, 0xc34000
	s_nop 0
	v_addc_co_u32_e32 v11, vcc, 0, v3, vcc
	v_add_co_u32_e32 v12, vcc, s1, v2
	s_mov_b32 s1, 0xc38000
	s_nop 0
	v_addc_co_u32_e32 v13, vcc, 0, v3, vcc
	global_load_dwordx4 v[134:137], v[10:11], off sc0 nt
	global_load_dwordx4 v[138:141], v[12:13], off sc0 nt
	v_add_co_u32_e32 v10, vcc, s1, v2
	s_mov_b32 s1, 0xc3c000
	s_nop 0
	v_addc_co_u32_e32 v11, vcc, 0, v3, vcc
	v_add_co_u32_e32 v12, vcc, s1, v2
	s_nop 1
	v_addc_co_u32_e32 v13, vcc, 0, v3, vcc
	global_load_dwordx4 v[146:149], v[10:11], off sc0 nt
	global_load_dwordx4 v[142:145], v[12:13], off sc0 nt
	ds_read_b128 v[10:13], v154 offset:34816
	ds_read_b128 v[18:21], v156 offset:34816
	ds_read_b128 v[26:29], v158 offset:34816
	ds_read_b128 v[42:45], v162 offset:34816
	s_waitcnt lgkmcnt(3)
	global_store_dwordx4 v[150:151], v[10:13], off offset:256 nt
	s_waitcnt lgkmcnt(2)
	global_store_dwordx4 v[152:153], v[18:21], off offset:256 nt
	s_waitcnt lgkmcnt(1)
	global_store_dwordx4 v[160:161], v[26:29], off offset:256 nt
	s_waitcnt lgkmcnt(0)
	global_store_dwordx4 v[164:165], v[42:45], off offset:256 nt
	s_waitcnt vmcnt(39)
	v_mul_f32_e32 v4, 0x43800000, v34
	s_waitcnt vmcnt(38)
	v_mul_f32_e32 v10, 0x43800000, v46
	v_med3_f32 v4, v4, s0, v1
	v_med3_f32 v12, v10, s0, v1
	v_mov_b32_e32 v10, v5
	v_cvt_pk_fp8_f32 v10, v4, v12
	s_waitcnt vmcnt(37)
	v_mul_f32_e32 v11, 0x43800000, v62
	s_waitcnt vmcnt(36)
	v_mul_f32_e32 v4, 0x43800000, v54
	v_med3_f32 v11, v11, s0, v1
	v_med3_f32 v4, v4, s0, v1
	v_cvt_pk_fp8_f32 v10, v11, v4 op_sel:[0,0,1]
	s_waitcnt vmcnt(35)
	v_mul_f32_e32 v4, 0x43800000, v66
	s_waitcnt vmcnt(34)
	v_mul_f32_e32 v11, 0x43800000, v78
	v_med3_f32 v4, v4, s0, v1
	v_med3_f32 v13, v11, s0, v1
	v_mov_b32_e32 v11, v5
	v_cvt_pk_fp8_f32 v11, v4, v13
	s_waitcnt vmcnt(33)
	v_mul_f32_e32 v12, 0x43800000, v94
	s_waitcnt vmcnt(32)
	v_mul_f32_e32 v4, 0x43800000, v86
	v_med3_f32 v12, v12, s0, v1
	v_med3_f32 v4, v4, s0, v1
	v_cvt_pk_fp8_f32 v11, v12, v4 op_sel:[0,0,1]
	s_waitcnt vmcnt(31)
	v_mul_f32_e32 v4, 0x43800000, v98
	s_waitcnt vmcnt(30)
	v_mul_f32_e32 v12, 0x43800000, v106
	v_med3_f32 v4, v4, s0, v1
	v_med3_f32 v18, v12, s0, v1
	v_mov_b32_e32 v12, v5
	v_cvt_pk_fp8_f32 v12, v4, v18
	s_waitcnt vmcnt(29)
	v_mul_f32_e32 v13, 0x43800000, v114
	s_waitcnt vmcnt(28)
	v_mul_f32_e32 v4, 0x43800000, v110
	v_med3_f32 v13, v13, s0, v1
	v_med3_f32 v4, v4, s0, v1
	v_cvt_pk_fp8_f32 v12, v13, v4 op_sel:[0,0,1]
	s_waitcnt vmcnt(27)
	v_mul_f32_e32 v4, 0x43800000, v118
	s_waitcnt vmcnt(26)
	v_mul_f32_e32 v13, 0x43800000, v122
	v_med3_f32 v4, v4, s0, v1
	v_med3_f32 v19, v13, s0, v1
	v_mov_b32_e32 v13, v5
	v_cvt_pk_fp8_f32 v13, v4, v19
	s_waitcnt vmcnt(25)
	v_mul_f32_e32 v18, 0x43800000, v130
	s_waitcnt vmcnt(24)
	v_mul_f32_e32 v4, 0x43800000, v126
	v_med3_f32 v18, v18, s0, v1
	v_med3_f32 v4, v4, s0, v1
	v_cvt_pk_fp8_f32 v13, v18, v4 op_sel:[0,0,1]
	v_mul_f32_e32 v4, 0x43800000, v35
	v_mul_f32_e32 v18, 0x43800000, v47
	v_med3_f32 v4, v4, s0, v1
	v_med3_f32 v20, v18, s0, v1
	v_mov_b32_e32 v18, v5
	v_cvt_pk_fp8_f32 v18, v4, v20
	v_mul_f32_e32 v19, 0x43800000, v63
	v_mul_f32_e32 v4, 0x43800000, v55
	v_med3_f32 v19, v19, s0, v1
	v_med3_f32 v4, v4, s0, v1
	v_cvt_pk_fp8_f32 v18, v19, v4 op_sel:[0,0,1]
	v_mul_f32_e32 v4, 0x43800000, v67
	v_mul_f32_e32 v19, 0x43800000, v79
	v_med3_f32 v4, v4, s0, v1
	v_med3_f32 v21, v19, s0, v1
	v_mov_b32_e32 v19, v5
	v_cvt_pk_fp8_f32 v19, v4, v21
	v_mul_f32_e32 v20, 0x43800000, v95
	v_mul_f32_e32 v4, 0x43800000, v87
	v_med3_f32 v20, v20, s0, v1
	v_med3_f32 v4, v4, s0, v1
	v_cvt_pk_fp8_f32 v19, v20, v4 op_sel:[0,0,1]
	v_mul_f32_e32 v4, 0x43800000, v99
	v_mul_f32_e32 v20, 0x43800000, v107
	v_med3_f32 v4, v4, s0, v1
	v_med3_f32 v26, v20, s0, v1
	v_mov_b32_e32 v20, v5
	v_cvt_pk_fp8_f32 v20, v4, v26
	v_mul_f32_e32 v21, 0x43800000, v115
	v_mul_f32_e32 v4, 0x43800000, v111
	v_med3_f32 v21, v21, s0, v1
	v_med3_f32 v4, v4, s0, v1
	v_cvt_pk_fp8_f32 v20, v21, v4 op_sel:[0,0,1]
	v_mul_f32_e32 v4, 0x43800000, v119
	v_mul_f32_e32 v21, 0x43800000, v123
	v_med3_f32 v4, v4, s0, v1
	v_med3_f32 v27, v21, s0, v1
	v_mov_b32_e32 v21, v5
	v_cvt_pk_fp8_f32 v21, v4, v27
	v_mul_f32_e32 v26, 0x43800000, v131
	v_mul_f32_e32 v4, 0x43800000, v127
	v_med3_f32 v26, v26, s0, v1
	v_med3_f32 v4, v4, s0, v1
	v_cvt_pk_fp8_f32 v21, v26, v4 op_sel:[0,0,1]
	v_mul_f32_e32 v4, 0x43800000, v36
	v_mul_f32_e32 v26, 0x43800000, v48
	v_med3_f32 v4, v4, s0, v1
	v_med3_f32 v28, v26, s0, v1
	v_mov_b32_e32 v26, v5
	v_cvt_pk_fp8_f32 v26, v4, v28
	v_mul_f32_e32 v27, 0x43800000, v64
	v_mul_f32_e32 v4, 0x43800000, v56
	v_med3_f32 v27, v27, s0, v1
	v_med3_f32 v4, v4, s0, v1
	v_cvt_pk_fp8_f32 v26, v27, v4 op_sel:[0,0,1]
	v_mul_f32_e32 v4, 0x43800000, v68
	v_mul_f32_e32 v27, 0x43800000, v80
	v_med3_f32 v4, v4, s0, v1
	v_med3_f32 v29, v27, s0, v1
	v_mov_b32_e32 v27, v5
	v_cvt_pk_fp8_f32 v27, v4, v29
	v_mul_f32_e32 v28, 0x43800000, v96
	v_mul_f32_e32 v4, 0x43800000, v88
	v_med3_f32 v28, v28, s0, v1
	v_med3_f32 v4, v4, s0, v1
	v_cvt_pk_fp8_f32 v27, v28, v4 op_sel:[0,0,1]
	v_mul_f32_e32 v4, 0x43800000, v100
	v_mul_f32_e32 v28, 0x43800000, v108
	v_med3_f32 v4, v4, s0, v1
	v_med3_f32 v34, v28, s0, v1
	v_mov_b32_e32 v28, v5
	v_cvt_pk_fp8_f32 v28, v4, v34
	v_mul_f32_e32 v29, 0x43800000, v116
	v_mul_f32_e32 v4, 0x43800000, v112
	v_med3_f32 v29, v29, s0, v1
	v_med3_f32 v4, v4, s0, v1
	v_cvt_pk_fp8_f32 v28, v29, v4 op_sel:[0,0,1]
	v_mul_f32_e32 v4, 0x43800000, v120
	v_mul_f32_e32 v29, 0x43800000, v124
	v_med3_f32 v4, v4, s0, v1
	v_med3_f32 v35, v29, s0, v1
	v_mov_b32_e32 v29, v5
	v_cvt_pk_fp8_f32 v29, v4, v35
	v_mul_f32_e32 v34, 0x43800000, v132
	v_mul_f32_e32 v4, 0x43800000, v128
	v_med3_f32 v34, v34, s0, v1
	v_med3_f32 v4, v4, s0, v1
	v_cvt_pk_fp8_f32 v29, v34, v4 op_sel:[0,0,1]
	v_mul_f32_e32 v4, 0x43800000, v37
	v_mul_f32_e32 v34, 0x43800000, v49
	v_med3_f32 v4, v4, s0, v1
	v_med3_f32 v36, v34, s0, v1
	v_mov_b32_e32 v34, v5
	v_cvt_pk_fp8_f32 v34, v4, v36
	v_mul_f32_e32 v35, 0x43800000, v65
	v_mul_f32_e32 v4, 0x43800000, v57
	v_med3_f32 v35, v35, s0, v1
	v_med3_f32 v4, v4, s0, v1
	v_cvt_pk_fp8_f32 v34, v35, v4 op_sel:[0,0,1]
	v_mul_f32_e32 v4, 0x43800000, v69
	v_mul_f32_e32 v35, 0x43800000, v81
	v_med3_f32 v4, v4, s0, v1
	v_med3_f32 v37, v35, s0, v1
	v_mov_b32_e32 v35, v5
	v_cvt_pk_fp8_f32 v35, v4, v37
	v_mul_f32_e32 v36, 0x43800000, v97
	v_mul_f32_e32 v4, 0x43800000, v89
	v_med3_f32 v36, v36, s0, v1
	v_med3_f32 v4, v4, s0, v1
	v_cvt_pk_fp8_f32 v35, v36, v4 op_sel:[0,0,1]
	v_mul_f32_e32 v4, 0x43800000, v101
	v_mul_f32_e32 v36, 0x43800000, v109
	v_med3_f32 v4, v4, s0, v1
	v_med3_f32 v42, v36, s0, v1
	v_mov_b32_e32 v36, v5
	v_cvt_pk_fp8_f32 v36, v4, v42
	v_mul_f32_e32 v37, 0x43800000, v117
	v_mul_f32_e32 v4, 0x43800000, v113
	v_med3_f32 v37, v37, s0, v1
	v_med3_f32 v4, v4, s0, v1
	v_cvt_pk_fp8_f32 v36, v37, v4 op_sel:[0,0,1]
	v_mul_f32_e32 v4, 0x43800000, v121
	v_mul_f32_e32 v37, 0x43800000, v125
	v_med3_f32 v4, v4, s0, v1
	v_med3_f32 v43, v37, s0, v1
	v_mov_b32_e32 v37, v5
	v_cvt_pk_fp8_f32 v37, v4, v43
	v_mul_f32_e32 v42, 0x43800000, v133
	v_mul_f32_e32 v4, 0x43800000, v129
	v_med3_f32 v42, v42, s0, v1
	v_med3_f32 v4, v4, s0, v1
	v_cvt_pk_fp8_f32 v37, v42, v4 op_sel:[0,0,1]
	ds_write_b128 v166, v[10:13]
	ds_write_b128 v166, v[18:21] offset:272
	ds_write_b128 v166, v[26:29] offset:544
	ds_write_b128 v166, v[34:37] offset:816
	s_waitcnt lgkmcnt(0)
	s_barrier
	s_mov_b32 s1, 0x1000000
	v_add_co_u32_e32 v10, vcc, s1, v2
	s_mov_b32 s1, 0x1004000
	s_nop 0
	v_addc_co_u32_e32 v11, vcc, 0, v3, vcc
	v_add_co_u32_e32 v18, vcc, s1, v2
	s_mov_b32 s1, 0x1008000
	s_nop 0
	v_addc_co_u32_e32 v19, vcc, 0, v3, vcc
	v_add_co_u32_e32 v26, vcc, s1, v2
	s_mov_b32 s1, 0x100c000
	s_nop 0
	v_addc_co_u32_e32 v27, vcc, 0, v3, vcc
	v_add_co_u32_e32 v28, vcc, s1, v2
	s_mov_b32 s1, 0x1010000
	s_nop 0
	v_addc_co_u32_e32 v29, vcc, 0, v3, vcc
	v_add_co_u32_e32 v42, vcc, s1, v2
	s_mov_b32 s1, 0x1014000
	s_nop 0
	v_addc_co_u32_e32 v43, vcc, 0, v3, vcc
	v_add_co_u32_e32 v46, vcc, s1, v2
	s_mov_b32 s1, 0x1018000
	s_nop 0
	v_addc_co_u32_e32 v47, vcc, 0, v3, vcc
	v_add_co_u32_e32 v54, vcc, s1, v2
	s_mov_b32 s1, 0x101c000
	s_nop 0
	v_addc_co_u32_e32 v55, vcc, 0, v3, vcc
	v_add_co_u32_e32 v56, vcc, s1, v2
	s_mov_b32 s1, 0x1020000
	s_nop 0
	v_addc_co_u32_e32 v57, vcc, 0, v3, vcc
	v_add_co_u32_e32 v66, vcc, s1, v2
	s_mov_b32 s1, 0x1024000
	s_nop 0
	v_addc_co_u32_e32 v67, vcc, 0, v3, vcc
	v_add_co_u32_e32 v78, vcc, s1, v2
	s_mov_b32 s1, 0x1028000
	s_nop 0
	v_addc_co_u32_e32 v79, vcc, 0, v3, vcc
	v_add_co_u32_e32 v86, vcc, s1, v2
	s_mov_b32 s1, 0x102c000
	s_nop 0
	v_addc_co_u32_e32 v87, vcc, 0, v3, vcc
	v_add_co_u32_e32 v88, vcc, s1, v2
	s_mov_b32 s1, 0x1030000
	s_nop 0
	v_addc_co_u32_e32 v89, vcc, 0, v3, vcc
	v_add_co_u32_e32 v98, vcc, s1, v2
	s_mov_b32 s1, 0x1034000
	s_nop 0
	v_addc_co_u32_e32 v99, vcc, 0, v3, vcc
	v_add_co_u32_e32 v106, vcc, s1, v2
	s_mov_b32 s1, 0x1038000
	s_nop 0
	v_addc_co_u32_e32 v107, vcc, 0, v3, vcc
	global_load_dwordx4 v[10:13], v[10:11], off sc0 nt
	s_nop 0
	global_load_dwordx4 v[18:21], v[18:19], off sc0 nt
	s_nop 0
	global_load_dwordx4 v[34:37], v[26:27], off sc0 nt
	s_nop 0
	global_load_dwordx4 v[26:29], v[28:29], off sc0 nt
	s_nop 0
	global_load_dwordx4 v[42:45], v[42:43], off sc0 nt
	s_nop 0
	global_load_dwordx4 v[46:49], v[46:47], off sc0 nt
	s_nop 0
	global_load_dwordx4 v[62:65], v[54:55], off sc0 nt
	s_nop 0
	global_load_dwordx4 v[54:57], v[56:57], off sc0 nt
	s_nop 0
	global_load_dwordx4 v[66:69], v[66:67], off sc0 nt
	s_nop 0
	global_load_dwordx4 v[78:81], v[78:79], off sc0 nt
	s_nop 0
	global_load_dwordx4 v[94:97], v[86:87], off sc0 nt
	s_nop 0
	global_load_dwordx4 v[86:89], v[88:89], off sc0 nt
	s_nop 0
	global_load_dwordx4 v[98:101], v[98:99], off sc0 nt
	s_nop 0
	global_load_dwordx4 v[110:113], v[106:107], off sc0 nt
	v_add_co_u32_e32 v106, vcc, s1, v2
	s_mov_b32 s1, 0x103c000
	s_nop 0
	v_addc_co_u32_e32 v107, vcc, 0, v3, vcc
	v_add_co_u32_e32 v108, vcc, s1, v2
	s_nop 1
	v_addc_co_u32_e32 v109, vcc, 0, v3, vcc
	global_load_dwordx4 v[126:129], v[106:107], off sc0 nt
	global_load_dwordx4 v[118:121], v[108:109], off sc0 nt
	ds_read_b128 v[106:109], v154
	ds_read_b128 v[114:117], v156
	ds_read_b128 v[122:125], v158
	ds_read_b128 v[130:133], v162
	s_waitcnt lgkmcnt(3)
	global_store_dwordx4 v[150:151], v[106:109], off offset:512 nt
	s_waitcnt lgkmcnt(2)
	global_store_dwordx4 v[152:153], v[114:117], off offset:512 nt
	s_waitcnt lgkmcnt(1)
	global_store_dwordx4 v[160:161], v[122:125], off offset:512 nt
	s_waitcnt lgkmcnt(0)
	global_store_dwordx4 v[164:165], v[130:133], off offset:512 nt
	s_waitcnt vmcnt(39)
	v_mul_f32_e32 v4, 0x43800000, v6
	s_waitcnt vmcnt(38)
	v_mul_f32_e32 v6, 0x43800000, v14
	v_med3_f32 v4, v4, s0, v1
	v_med3_f32 v6, v6, s0, v1
	v_mov_b32_e32 v106, v5
	v_cvt_pk_fp8_f32 v106, v4, v6
	s_waitcnt vmcnt(37)
	v_mul_f32_e32 v14, 0x43800000, v30
	s_waitcnt vmcnt(36)
	v_mul_f32_e32 v4, 0x43800000, v22
	v_med3_f32 v6, v14, s0, v1
	v_med3_f32 v4, v4, s0, v1
	v_cvt_pk_fp8_f32 v106, v6, v4 op_sel:[0,0,1]
	s_waitcnt vmcnt(35)
	v_mul_f32_e32 v4, 0x43800000, v38
	s_waitcnt vmcnt(34)
	v_mul_f32_e32 v6, 0x43800000, v50
	v_med3_f32 v4, v4, s0, v1
	v_med3_f32 v6, v6, s0, v1
	v_mov_b32_e32 v107, v5
	v_cvt_pk_fp8_f32 v107, v4, v6
	s_waitcnt vmcnt(33)
	v_mul_f32_e32 v14, 0x43800000, v70
	s_waitcnt vmcnt(32)
	v_mul_f32_e32 v4, 0x43800000, v58
	v_med3_f32 v6, v14, s0, v1
	v_med3_f32 v4, v4, s0, v1
	v_cvt_pk_fp8_f32 v107, v6, v4 op_sel:[0,0,1]
	s_waitcnt vmcnt(31)
	v_mul_f32_e32 v4, 0x43800000, v74
	s_waitcnt vmcnt(30)
	v_mul_f32_e32 v6, 0x43800000, v82
	v_med3_f32 v4, v4, s0, v1
	v_med3_f32 v6, v6, s0, v1
	v_mov_b32_e32 v108, v5
	v_cvt_pk_fp8_f32 v108, v4, v6
	s_waitcnt vmcnt(29)
	v_mul_f32_e32 v14, 0x43800000, v102
	s_waitcnt vmcnt(28)
	v_mul_f32_e32 v4, 0x43800000, v90
	v_med3_f32 v6, v14, s0, v1
	v_med3_f32 v4, v4, s0, v1
	v_cvt_pk_fp8_f32 v108, v6, v4 op_sel:[0,0,1]
	s_waitcnt vmcnt(27)
	v_mul_f32_e32 v4, 0x43800000, v134
	s_waitcnt vmcnt(26)
	v_mul_f32_e32 v6, 0x43800000, v138
	v_med3_f32 v4, v4, s0, v1
	v_med3_f32 v6, v6, s0, v1
	v_mov_b32_e32 v109, v5
	v_cvt_pk_fp8_f32 v109, v4, v6
	s_waitcnt vmcnt(25)
	v_mul_f32_e32 v14, 0x43800000, v146
	s_waitcnt vmcnt(24)
	v_mul_f32_e32 v4, 0x43800000, v142
	v_med3_f32 v6, v14, s0, v1
	v_med3_f32 v4, v4, s0, v1
	v_cvt_pk_fp8_f32 v109, v6, v4 op_sel:[0,0,1]
	v_mul_f32_e32 v4, 0x43800000, v7
	v_mul_f32_e32 v6, 0x43800000, v15
	v_med3_f32 v4, v4, s0, v1
	v_med3_f32 v6, v6, s0, v1
	v_mov_b32_e32 v114, v5
	v_cvt_pk_fp8_f32 v114, v4, v6
	v_mul_f32_e32 v7, 0x43800000, v31
	v_mul_f32_e32 v4, 0x43800000, v23
	v_med3_f32 v6, v7, s0, v1
	v_med3_f32 v4, v4, s0, v1
	v_cvt_pk_fp8_f32 v114, v6, v4 op_sel:[0,0,1]
	v_mul_f32_e32 v4, 0x43800000, v39
	v_mul_f32_e32 v6, 0x43800000, v51
	v_med3_f32 v4, v4, s0, v1
	v_med3_f32 v6, v6, s0, v1
	v_mov_b32_e32 v115, v5
	v_cvt_pk_fp8_f32 v115, v4, v6
	v_mul_f32_e32 v7, 0x43800000, v71
	v_mul_f32_e32 v4, 0x43800000, v59
	v_med3_f32 v6, v7, s0, v1
	v_med3_f32 v4, v4, s0, v1
	v_cvt_pk_fp8_f32 v115, v6, v4 op_sel:[0,0,1]
	v_mul_f32_e32 v4, 0x43800000, v75
	v_mul_f32_e32 v6, 0x43800000, v83
	v_med3_f32 v4, v4, s0, v1
	v_med3_f32 v6, v6, s0, v1
	v_mov_b32_e32 v116, v5
	v_cvt_pk_fp8_f32 v116, v4, v6
	v_mul_f32_e32 v7, 0x43800000, v103
	v_mul_f32_e32 v4, 0x43800000, v91
	v_med3_f32 v6, v7, s0, v1
	v_med3_f32 v4, v4, s0, v1
	v_cvt_pk_fp8_f32 v116, v6, v4 op_sel:[0,0,1]
	v_mul_f32_e32 v4, 0x43800000, v135
	v_mul_f32_e32 v6, 0x43800000, v139
	v_med3_f32 v4, v4, s0, v1
	v_med3_f32 v6, v6, s0, v1
	v_mov_b32_e32 v117, v5
	v_cvt_pk_fp8_f32 v117, v4, v6
	v_mul_f32_e32 v7, 0x43800000, v147
	v_mul_f32_e32 v4, 0x43800000, v143
	v_med3_f32 v6, v7, s0, v1
	v_med3_f32 v4, v4, s0, v1
	v_cvt_pk_fp8_f32 v117, v6, v4 op_sel:[0,0,1]
	v_mul_f32_e32 v4, 0x43800000, v8
	v_mul_f32_e32 v6, 0x43800000, v16
	v_med3_f32 v4, v4, s0, v1
	v_med3_f32 v6, v6, s0, v1
	v_mov_b32_e32 v122, v5
	v_cvt_pk_fp8_f32 v122, v4, v6
	v_mul_f32_e32 v7, 0x43800000, v32
	v_mul_f32_e32 v4, 0x43800000, v24
	v_med3_f32 v6, v7, s0, v1
	v_med3_f32 v4, v4, s0, v1
	v_cvt_pk_fp8_f32 v122, v6, v4 op_sel:[0,0,1]
	v_mul_f32_e32 v4, 0x43800000, v40
	v_mul_f32_e32 v6, 0x43800000, v52
	v_med3_f32 v4, v4, s0, v1
	v_med3_f32 v6, v6, s0, v1
	v_mov_b32_e32 v123, v5
	v_cvt_pk_fp8_f32 v123, v4, v6
	v_mul_f32_e32 v7, 0x43800000, v72
	v_mul_f32_e32 v4, 0x43800000, v60
	v_med3_f32 v6, v7, s0, v1
	v_med3_f32 v4, v4, s0, v1
	v_cvt_pk_fp8_f32 v123, v6, v4 op_sel:[0,0,1]
	v_mul_f32_e32 v4, 0x43800000, v76
	v_mul_f32_e32 v6, 0x43800000, v84
	v_med3_f32 v4, v4, s0, v1
	v_med3_f32 v6, v6, s0, v1
	v_mov_b32_e32 v124, v5
	v_cvt_pk_fp8_f32 v124, v4, v6
	v_mul_f32_e32 v7, 0x43800000, v104
	v_mul_f32_e32 v4, 0x43800000, v92
	v_med3_f32 v6, v7, s0, v1
	v_med3_f32 v4, v4, s0, v1
	v_cvt_pk_fp8_f32 v124, v6, v4 op_sel:[0,0,1]
	v_mul_f32_e32 v4, 0x43800000, v136
	v_mul_f32_e32 v6, 0x43800000, v140
	v_med3_f32 v4, v4, s0, v1
	v_med3_f32 v6, v6, s0, v1
	v_mov_b32_e32 v125, v5
	v_cvt_pk_fp8_f32 v125, v4, v6
	v_mul_f32_e32 v7, 0x43800000, v148
	v_mul_f32_e32 v4, 0x43800000, v144
	v_med3_f32 v6, v7, s0, v1
	v_med3_f32 v4, v4, s0, v1
	v_cvt_pk_fp8_f32 v125, v6, v4 op_sel:[0,0,1]
	v_mul_f32_e32 v4, 0x43800000, v9
	v_mul_f32_e32 v6, 0x43800000, v17
	v_med3_f32 v4, v4, s0, v1
	v_med3_f32 v8, v6, s0, v1
	v_mov_b32_e32 v6, v5
	v_cvt_pk_fp8_f32 v6, v4, v8
	v_mul_f32_e32 v7, 0x43800000, v33
	v_mul_f32_e32 v4, 0x43800000, v25
	v_med3_f32 v7, v7, s0, v1
	v_med3_f32 v4, v4, s0, v1
	v_cvt_pk_fp8_f32 v6, v7, v4 op_sel:[0,0,1]
	v_mul_f32_e32 v4, 0x43800000, v41
	v_mul_f32_e32 v7, 0x43800000, v53
	v_med3_f32 v4, v4, s0, v1
	v_med3_f32 v9, v7, s0, v1
	v_mov_b32_e32 v7, v5
	v_cvt_pk_fp8_f32 v7, v4, v9
	v_mul_f32_e32 v8, 0x43800000, v73
	v_mul_f32_e32 v4, 0x43800000, v61
	v_med3_f32 v8, v8, s0, v1
	v_med3_f32 v4, v4, s0, v1
	v_cvt_pk_fp8_f32 v7, v8, v4 op_sel:[0,0,1]
	v_mul_f32_e32 v4, 0x43800000, v77
	v_mul_f32_e32 v8, 0x43800000, v85
	v_med3_f32 v4, v4, s0, v1
	v_med3_f32 v14, v8, s0, v1
	v_mov_b32_e32 v8, v5
	v_cvt_pk_fp8_f32 v8, v4, v14
	v_mul_f32_e32 v9, 0x43800000, v105
	v_mul_f32_e32 v4, 0x43800000, v93
	v_med3_f32 v9, v9, s0, v1
	v_med3_f32 v4, v4, s0, v1
	v_cvt_pk_fp8_f32 v8, v9, v4 op_sel:[0,0,1]
	v_mul_f32_e32 v4, 0x43800000, v137
	v_mul_f32_e32 v9, 0x43800000, v141
	v_med3_f32 v4, v4, s0, v1
	v_med3_f32 v15, v9, s0, v1
	v_mov_b32_e32 v9, v5
	v_cvt_pk_fp8_f32 v9, v4, v15
	v_mul_f32_e32 v14, 0x43800000, v149
	v_mul_f32_e32 v4, 0x43800000, v145
	v_med3_f32 v14, v14, s0, v1
	v_med3_f32 v4, v4, s0, v1
	v_cvt_pk_fp8_f32 v9, v14, v4 op_sel:[0,0,1]
	ds_write_b128 v166, v[106:109] offset:34816
	ds_write_b128 v166, v[114:117] offset:35088
	ds_write_b128 v166, v[122:125] offset:35360
	ds_write_b128 v166, v[6:9] offset:35632
	s_waitcnt lgkmcnt(0)
	s_barrier
	s_mov_b32 s1, 0x1400000
	v_add_co_u32_e32 v6, vcc, s1, v2
	s_mov_b32 s1, 0x1404000
	s_nop 0
	v_addc_co_u32_e32 v7, vcc, 0, v3, vcc
	v_add_co_u32_e32 v14, vcc, s1, v2
	s_mov_b32 s1, 0x1408000
	s_nop 0
	v_addc_co_u32_e32 v15, vcc, 0, v3, vcc
	v_add_co_u32_e32 v22, vcc, s1, v2
	s_mov_b32 s1, 0x140c000
	s_nop 0
	v_addc_co_u32_e32 v23, vcc, 0, v3, vcc
	v_add_co_u32_e32 v24, vcc, s1, v2
	s_mov_b32 s1, 0x1410000
	s_nop 0
	v_addc_co_u32_e32 v25, vcc, 0, v3, vcc
	v_add_co_u32_e32 v38, vcc, s1, v2
	s_mov_b32 s1, 0x1414000
	s_nop 0
	v_addc_co_u32_e32 v39, vcc, 0, v3, vcc
	v_add_co_u32_e32 v50, vcc, s1, v2
	s_mov_b32 s1, 0x1418000
	s_nop 0
	v_addc_co_u32_e32 v51, vcc, 0, v3, vcc
	v_add_co_u32_e32 v58, vcc, s1, v2
	s_mov_b32 s1, 0x141c000
	s_nop 0
	v_addc_co_u32_e32 v59, vcc, 0, v3, vcc
	v_add_co_u32_e32 v60, vcc, s1, v2
	s_mov_b32 s1, 0x1420000
	s_nop 0
	v_addc_co_u32_e32 v61, vcc, 0, v3, vcc
	v_add_co_u32_e32 v74, vcc, s1, v2
	s_mov_b32 s1, 0x1424000
	s_nop 0
	v_addc_co_u32_e32 v75, vcc, 0, v3, vcc
	v_add_co_u32_e32 v82, vcc, s1, v2
	s_mov_b32 s1, 0x1428000
	s_nop 0
	v_addc_co_u32_e32 v83, vcc, 0, v3, vcc
	v_add_co_u32_e32 v90, vcc, s1, v2
	s_mov_b32 s1, 0x142c000
	s_nop 0
	v_addc_co_u32_e32 v91, vcc, 0, v3, vcc
	v_add_co_u32_e32 v92, vcc, s1, v2
	s_mov_b32 s1, 0x1430000
	s_nop 0
	v_addc_co_u32_e32 v93, vcc, 0, v3, vcc
	v_add_co_u32_e32 v106, vcc, s1, v2
	s_mov_b32 s1, 0x1434000
	s_nop 0
	v_addc_co_u32_e32 v107, vcc, 0, v3, vcc
	v_add_co_u32_e32 v114, vcc, s1, v2
	s_mov_b32 s1, 0x1438000
	s_nop 0
	v_addc_co_u32_e32 v115, vcc, 0, v3, vcc
	v_add_co_u32_e32 v122, vcc, s1, v2
	s_mov_b32 s1, 0x143c000
	s_nop 0
	v_addc_co_u32_e32 v123, vcc, 0, v3, vcc
	v_add_co_u32_e32 v124, vcc, s1, v2
	global_load_dwordx4 v[6:9], v[6:7], off sc0 nt
	s_nop 0
	global_load_dwordx4 v[14:17], v[14:15], off sc0 nt
	v_addc_co_u32_e32 v125, vcc, 0, v3, vcc
	global_load_dwordx4 v[30:33], v[22:23], off sc0 nt
	s_nop 0
	global_load_dwordx4 v[22:25], v[24:25], off sc0 nt
	s_nop 0
	global_load_dwordx4 v[38:41], v[38:39], off sc0 nt
	s_nop 0
	global_load_dwordx4 v[50:53], v[50:51], off sc0 nt
	s_nop 0
	global_load_dwordx4 v[70:73], v[58:59], off sc0 nt
	s_nop 0
	global_load_dwordx4 v[58:61], v[60:61], off sc0 nt
	s_nop 0
	global_load_dwordx4 v[74:77], v[74:75], off sc0 nt
	s_nop 0
	global_load_dwordx4 v[82:85], v[82:83], off sc0 nt
	s_nop 0
	global_load_dwordx4 v[102:105], v[90:91], off sc0 nt
	s_nop 0
	global_load_dwordx4 v[90:93], v[92:93], off sc0 nt
	s_nop 0
	global_load_dwordx4 v[106:109], v[106:107], off sc0 nt
	s_nop 0
	global_load_dwordx4 v[114:117], v[114:115], off sc0 nt
	s_nop 0
	global_load_dwordx4 v[130:133], v[122:123], off sc0 nt
	s_nop 0
	global_load_dwordx4 v[122:125], v[124:125], off sc0 nt
	ds_read_b128 v[134:137], v154 offset:34816
	ds_read_b128 v[138:141], v156 offset:34816
	ds_read_b128 v[142:145], v158 offset:34816
	ds_read_b128 v[146:149], v162 offset:34816
	s_waitcnt lgkmcnt(3)
	global_store_dwordx4 v[150:151], v[134:137], off offset:768 nt
	s_waitcnt lgkmcnt(2)
	global_store_dwordx4 v[152:153], v[138:141], off offset:768 nt
	s_waitcnt lgkmcnt(1)
	global_store_dwordx4 v[160:161], v[142:145], off offset:768 nt
	s_waitcnt lgkmcnt(0)
	global_store_dwordx4 v[164:165], v[146:149], off offset:768 nt
	s_waitcnt vmcnt(39)
	v_mul_f32_e32 v4, 0x43800000, v10
	s_waitcnt vmcnt(38)
	v_mul_f32_e32 v10, 0x43800000, v18
	v_med3_f32 v4, v4, s0, v1
	v_med3_f32 v10, v10, s0, v1
	v_mov_b32_e32 v134, v5
	v_cvt_pk_fp8_f32 v134, v4, v10
	s_waitcnt vmcnt(37)
	v_mul_f32_e32 v18, 0x43800000, v34
	s_waitcnt vmcnt(36)
	v_mul_f32_e32 v4, 0x43800000, v26
	v_med3_f32 v10, v18, s0, v1
	v_med3_f32 v4, v4, s0, v1
	v_cvt_pk_fp8_f32 v134, v10, v4 op_sel:[0,0,1]
	s_waitcnt vmcnt(35)
	v_mul_f32_e32 v4, 0x43800000, v42
	s_waitcnt vmcnt(34)
	v_mul_f32_e32 v10, 0x43800000, v46
	v_med3_f32 v4, v4, s0, v1
	v_med3_f32 v10, v10, s0, v1
	v_mov_b32_e32 v135, v5
	v_cvt_pk_fp8_f32 v135, v4, v10
	s_waitcnt vmcnt(33)
	v_mul_f32_e32 v18, 0x43800000, v62
	s_waitcnt vmcnt(32)
	v_mul_f32_e32 v4, 0x43800000, v54
	v_med3_f32 v10, v18, s0, v1
	v_med3_f32 v4, v4, s0, v1
	v_cvt_pk_fp8_f32 v135, v10, v4 op_sel:[0,0,1]
	s_waitcnt vmcnt(31)
	v_mul_f32_e32 v4, 0x43800000, v66
	s_waitcnt vmcnt(30)
	v_mul_f32_e32 v10, 0x43800000, v78
	v_med3_f32 v4, v4, s0, v1
	v_med3_f32 v10, v10, s0, v1
	v_mov_b32_e32 v136, v5
	v_cvt_pk_fp8_f32 v136, v4, v10
	s_waitcnt vmcnt(29)
	v_mul_f32_e32 v18, 0x43800000, v94
	s_waitcnt vmcnt(28)
	v_mul_f32_e32 v4, 0x43800000, v86
	v_med3_f32 v10, v18, s0, v1
	v_med3_f32 v4, v4, s0, v1
	v_cvt_pk_fp8_f32 v136, v10, v4 op_sel:[0,0,1]
	s_waitcnt vmcnt(27)
	v_mul_f32_e32 v4, 0x43800000, v98
	s_waitcnt vmcnt(26)
	v_mul_f32_e32 v10, 0x43800000, v110
	v_med3_f32 v4, v4, s0, v1
	v_med3_f32 v10, v10, s0, v1
	v_mov_b32_e32 v137, v5
	v_cvt_pk_fp8_f32 v137, v4, v10
	s_waitcnt vmcnt(25)
	v_mul_f32_e32 v18, 0x43800000, v126
	s_waitcnt vmcnt(24)
	v_mul_f32_e32 v4, 0x43800000, v118
	v_med3_f32 v10, v18, s0, v1
	v_med3_f32 v4, v4, s0, v1
	v_cvt_pk_fp8_f32 v137, v10, v4 op_sel:[0,0,1]
	v_mul_f32_e32 v4, 0x43800000, v11
	v_mul_f32_e32 v10, 0x43800000, v19
	v_med3_f32 v4, v4, s0, v1
	v_med3_f32 v10, v10, s0, v1
	v_mov_b32_e32 v138, v5
	v_cvt_pk_fp8_f32 v138, v4, v10
	v_mul_f32_e32 v11, 0x43800000, v35
	v_mul_f32_e32 v4, 0x43800000, v27
	v_med3_f32 v10, v11, s0, v1
	v_med3_f32 v4, v4, s0, v1
	v_cvt_pk_fp8_f32 v138, v10, v4 op_sel:[0,0,1]
	v_mul_f32_e32 v4, 0x43800000, v43
	v_mul_f32_e32 v10, 0x43800000, v47
	v_med3_f32 v4, v4, s0, v1
	v_med3_f32 v10, v10, s0, v1
	v_mov_b32_e32 v139, v5
	v_cvt_pk_fp8_f32 v139, v4, v10
	v_mul_f32_e32 v11, 0x43800000, v63
	v_mul_f32_e32 v4, 0x43800000, v55
	v_med3_f32 v10, v11, s0, v1
	v_med3_f32 v4, v4, s0, v1
	v_cvt_pk_fp8_f32 v139, v10, v4 op_sel:[0,0,1]
	v_mul_f32_e32 v4, 0x43800000, v67
	v_mul_f32_e32 v10, 0x43800000, v79
	v_med3_f32 v4, v4, s0, v1
	v_med3_f32 v10, v10, s0, v1
	v_mov_b32_e32 v140, v5
	v_cvt_pk_fp8_f32 v140, v4, v10
	v_mul_f32_e32 v11, 0x43800000, v95
	v_mul_f32_e32 v4, 0x43800000, v87
	v_med3_f32 v10, v11, s0, v1
	v_med3_f32 v4, v4, s0, v1
	v_cvt_pk_fp8_f32 v140, v10, v4 op_sel:[0,0,1]
	v_mul_f32_e32 v4, 0x43800000, v99
	v_mul_f32_e32 v10, 0x43800000, v111
	v_med3_f32 v4, v4, s0, v1
	v_med3_f32 v10, v10, s0, v1
	v_mov_b32_e32 v141, v5
	v_cvt_pk_fp8_f32 v141, v4, v10
	v_mul_f32_e32 v11, 0x43800000, v127
	v_mul_f32_e32 v4, 0x43800000, v119
	v_med3_f32 v10, v11, s0, v1
	v_med3_f32 v4, v4, s0, v1
	v_cvt_pk_fp8_f32 v141, v10, v4 op_sel:[0,0,1]
	v_mul_f32_e32 v4, 0x43800000, v12
	v_mul_f32_e32 v10, 0x43800000, v20
	v_med3_f32 v4, v4, s0, v1
	v_med3_f32 v10, v10, s0, v1
	v_mov_b32_e32 v142, v5
	v_cvt_pk_fp8_f32 v142, v4, v10
	v_mul_f32_e32 v11, 0x43800000, v36
	v_mul_f32_e32 v4, 0x43800000, v28
	v_med3_f32 v10, v11, s0, v1
	v_med3_f32 v4, v4, s0, v1
	v_cvt_pk_fp8_f32 v142, v10, v4 op_sel:[0,0,1]
	v_mul_f32_e32 v4, 0x43800000, v44
	v_mul_f32_e32 v10, 0x43800000, v48
	v_med3_f32 v4, v4, s0, v1
	v_med3_f32 v10, v10, s0, v1
	v_mov_b32_e32 v143, v5
	v_cvt_pk_fp8_f32 v143, v4, v10
	v_mul_f32_e32 v11, 0x43800000, v64
	v_mul_f32_e32 v4, 0x43800000, v56
	v_med3_f32 v10, v11, s0, v1
	v_med3_f32 v4, v4, s0, v1
	v_cvt_pk_fp8_f32 v143, v10, v4 op_sel:[0,0,1]
	v_mul_f32_e32 v4, 0x43800000, v68
	v_mul_f32_e32 v10, 0x43800000, v80
	v_med3_f32 v4, v4, s0, v1
	v_med3_f32 v10, v10, s0, v1
	v_mov_b32_e32 v144, v5
	v_cvt_pk_fp8_f32 v144, v4, v10
	v_mul_f32_e32 v11, 0x43800000, v96
	v_mul_f32_e32 v4, 0x43800000, v88
	v_med3_f32 v10, v11, s0, v1
	v_med3_f32 v4, v4, s0, v1
	v_cvt_pk_fp8_f32 v144, v10, v4 op_sel:[0,0,1]
	v_mul_f32_e32 v4, 0x43800000, v100
	v_mul_f32_e32 v10, 0x43800000, v112
	v_med3_f32 v4, v4, s0, v1
	v_med3_f32 v10, v10, s0, v1
	v_mov_b32_e32 v145, v5
	v_cvt_pk_fp8_f32 v145, v4, v10
	v_mul_f32_e32 v11, 0x43800000, v128
	v_mul_f32_e32 v4, 0x43800000, v120
	v_med3_f32 v10, v11, s0, v1
	v_med3_f32 v4, v4, s0, v1
	v_cvt_pk_fp8_f32 v145, v10, v4 op_sel:[0,0,1]
	v_mul_f32_e32 v4, 0x43800000, v13
	v_mul_f32_e32 v10, 0x43800000, v21
	v_med3_f32 v4, v4, s0, v1
	v_med3_f32 v12, v10, s0, v1
	v_mov_b32_e32 v10, v5
	v_cvt_pk_fp8_f32 v10, v4, v12
	v_mul_f32_e32 v11, 0x43800000, v37
	v_mul_f32_e32 v4, 0x43800000, v29
	v_med3_f32 v11, v11, s0, v1
	v_med3_f32 v4, v4, s0, v1
	v_cvt_pk_fp8_f32 v10, v11, v4 op_sel:[0,0,1]
	v_mul_f32_e32 v4, 0x43800000, v45
	v_mul_f32_e32 v11, 0x43800000, v49
	v_med3_f32 v4, v4, s0, v1
	v_med3_f32 v13, v11, s0, v1
	v_mov_b32_e32 v11, v5
	v_cvt_pk_fp8_f32 v11, v4, v13
	v_mul_f32_e32 v12, 0x43800000, v65
	v_mul_f32_e32 v4, 0x43800000, v57
	v_med3_f32 v12, v12, s0, v1
	v_med3_f32 v4, v4, s0, v1
	v_cvt_pk_fp8_f32 v11, v12, v4 op_sel:[0,0,1]
	v_mul_f32_e32 v4, 0x43800000, v69
	v_mul_f32_e32 v12, 0x43800000, v81
	v_med3_f32 v4, v4, s0, v1
	v_med3_f32 v18, v12, s0, v1
	v_mov_b32_e32 v12, v5
	v_cvt_pk_fp8_f32 v12, v4, v18
	v_mul_f32_e32 v13, 0x43800000, v97
	v_mul_f32_e32 v4, 0x43800000, v89
	v_med3_f32 v13, v13, s0, v1
	v_med3_f32 v4, v4, s0, v1
	v_cvt_pk_fp8_f32 v12, v13, v4 op_sel:[0,0,1]
	v_mul_f32_e32 v4, 0x43800000, v101
	v_mul_f32_e32 v13, 0x43800000, v113
	v_med3_f32 v4, v4, s0, v1
	v_med3_f32 v19, v13, s0, v1
	v_mov_b32_e32 v13, v5
	v_cvt_pk_fp8_f32 v13, v4, v19
	v_mul_f32_e32 v18, 0x43800000, v129
	v_mul_f32_e32 v4, 0x43800000, v121
	v_med3_f32 v18, v18, s0, v1
	v_med3_f32 v4, v4, s0, v1
	v_cvt_pk_fp8_f32 v13, v18, v4 op_sel:[0,0,1]
	ds_write_b128 v166, v[134:137]
	ds_write_b128 v166, v[138:141] offset:272
	ds_write_b128 v166, v[142:145] offset:544
	ds_write_b128 v166, v[10:13] offset:816
	s_waitcnt lgkmcnt(0)
	s_barrier
	s_mov_b32 s1, 0x1800000
	v_add_co_u32_e32 v10, vcc, s1, v2
	s_mov_b32 s1, 0x1804000
	s_nop 0
	v_addc_co_u32_e32 v11, vcc, 0, v3, vcc
	v_add_co_u32_e32 v18, vcc, s1, v2
	s_mov_b32 s1, 0x1808000
	s_nop 0
	v_addc_co_u32_e32 v19, vcc, 0, v3, vcc
	v_add_co_u32_e32 v26, vcc, s1, v2
	s_mov_b32 s1, 0x180c000
	s_nop 0
	v_addc_co_u32_e32 v27, vcc, 0, v3, vcc
	v_add_co_u32_e32 v28, vcc, s1, v2
	s_mov_b32 s1, 0x1810000
	s_nop 0
	v_addc_co_u32_e32 v29, vcc, 0, v3, vcc
	v_add_co_u32_e32 v42, vcc, s1, v2
	s_mov_b32 s1, 0x1814000
	s_nop 0
	v_addc_co_u32_e32 v43, vcc, 0, v3, vcc
	v_add_co_u32_e32 v46, vcc, s1, v2
	s_mov_b32 s1, 0x1818000
	s_nop 0
	v_addc_co_u32_e32 v47, vcc, 0, v3, vcc
	v_add_co_u32_e32 v54, vcc, s1, v2
	s_mov_b32 s1, 0x181c000
	s_nop 0
	v_addc_co_u32_e32 v55, vcc, 0, v3, vcc
	v_add_co_u32_e32 v56, vcc, s1, v2
	s_mov_b32 s1, 0x1820000
	s_nop 0
	v_addc_co_u32_e32 v57, vcc, 0, v3, vcc
	v_add_co_u32_e32 v66, vcc, s1, v2
	s_mov_b32 s1, 0x1824000
	s_nop 0
	v_addc_co_u32_e32 v67, vcc, 0, v3, vcc
	v_add_co_u32_e32 v78, vcc, s1, v2
	s_mov_b32 s1, 0x1828000
	s_nop 0
	v_addc_co_u32_e32 v79, vcc, 0, v3, vcc
	v_add_co_u32_e32 v86, vcc, s1, v2
	s_mov_b32 s1, 0x182c000
	s_nop 0
	v_addc_co_u32_e32 v87, vcc, 0, v3, vcc
	v_add_co_u32_e32 v88, vcc, s1, v2
	s_mov_b32 s1, 0x1830000
	s_nop 0
	v_addc_co_u32_e32 v89, vcc, 0, v3, vcc
	v_add_co_u32_e32 v98, vcc, s1, v2
	s_mov_b32 s1, 0x1834000
	s_nop 0
	v_addc_co_u32_e32 v99, vcc, 0, v3, vcc
	v_add_co_u32_e32 v110, vcc, s1, v2
	s_mov_b32 s1, 0x1838000
	s_nop 0
	v_addc_co_u32_e32 v111, vcc, 0, v3, vcc
	v_add_co_u32_e32 v118, vcc, s1, v2
	s_mov_b32 s1, 0x183c000
	s_nop 0
	v_addc_co_u32_e32 v119, vcc, 0, v3, vcc
	v_add_co_u32_e32 v120, vcc, s1, v2
	global_load_dwordx4 v[10:13], v[10:11], off sc0 nt
	s_nop 0
	global_load_dwordx4 v[18:21], v[18:19], off sc0 nt
	v_addc_co_u32_e32 v121, vcc, 0, v3, vcc
	global_load_dwordx4 v[34:37], v[26:27], off sc0 nt
	s_nop 0
	global_load_dwordx4 v[26:29], v[28:29], off sc0 nt
	s_nop 0
	global_load_dwordx4 v[42:45], v[42:43], off sc0 nt
	s_nop 0
	global_load_dwordx4 v[46:49], v[46:47], off sc0 nt
	s_nop 0
	global_load_dwordx4 v[62:65], v[54:55], off sc0 nt
	s_nop 0
	global_load_dwordx4 v[54:57], v[56:57], off sc0 nt
	s_nop 0
	global_load_dwordx4 v[66:69], v[66:67], off sc0 nt
	s_nop 0
	global_load_dwordx4 v[78:81], v[78:79], off sc0 nt
	s_nop 0
	global_load_dwordx4 v[94:97], v[86:87], off sc0 nt
	s_nop 0
	global_load_dwordx4 v[86:89], v[88:89], off sc0 nt
	s_nop 0
	global_load_dwordx4 v[98:101], v[98:99], off sc0 nt
	s_nop 0
	global_load_dwordx4 v[110:113], v[110:111], off sc0 nt
	s_nop 0
	global_load_dwordx4 v[126:129], v[118:119], off sc0 nt
	s_nop 0
	global_load_dwordx4 v[118:121], v[120:121], off sc0 nt
	ds_read_b128 v[134:137], v154
	ds_read_b128 v[138:141], v156
	ds_read_b128 v[142:145], v158
	ds_read_b128 v[146:149], v162
	s_waitcnt lgkmcnt(3)
	global_store_dwordx4 v[150:151], v[134:137], off offset:1024 nt
	s_waitcnt lgkmcnt(2)
	global_store_dwordx4 v[152:153], v[138:141], off offset:1024 nt
	s_waitcnt lgkmcnt(1)
	global_store_dwordx4 v[160:161], v[142:145], off offset:1024 nt
	s_waitcnt lgkmcnt(0)
	global_store_dwordx4 v[164:165], v[146:149], off offset:1024 nt
	s_waitcnt vmcnt(39)
	v_mul_f32_e32 v4, 0x43800000, v6
	s_waitcnt vmcnt(38)
	v_mul_f32_e32 v6, 0x43800000, v14
	v_med3_f32 v4, v4, s0, v1
	v_med3_f32 v6, v6, s0, v1
	v_mov_b32_e32 v134, v5
	v_cvt_pk_fp8_f32 v134, v4, v6
	s_waitcnt vmcnt(37)
	v_mul_f32_e32 v14, 0x43800000, v30
	s_waitcnt vmcnt(36)
	v_mul_f32_e32 v4, 0x43800000, v22
	v_med3_f32 v6, v14, s0, v1
	v_med3_f32 v4, v4, s0, v1
	v_cvt_pk_fp8_f32 v134, v6, v4 op_sel:[0,0,1]
	s_waitcnt vmcnt(35)
	v_mul_f32_e32 v4, 0x43800000, v38
	s_waitcnt vmcnt(34)
	v_mul_f32_e32 v6, 0x43800000, v50
	v_med3_f32 v4, v4, s0, v1
	v_med3_f32 v6, v6, s0, v1
	v_mov_b32_e32 v135, v5
	v_cvt_pk_fp8_f32 v135, v4, v6
	s_waitcnt vmcnt(33)
	v_mul_f32_e32 v14, 0x43800000, v70
	s_waitcnt vmcnt(32)
	v_mul_f32_e32 v4, 0x43800000, v58
	v_med3_f32 v6, v14, s0, v1
	v_med3_f32 v4, v4, s0, v1
	v_cvt_pk_fp8_f32 v135, v6, v4 op_sel:[0,0,1]
	s_waitcnt vmcnt(31)
	v_mul_f32_e32 v4, 0x43800000, v74
	s_waitcnt vmcnt(30)
	v_mul_f32_e32 v6, 0x43800000, v82
	v_med3_f32 v4, v4, s0, v1
	v_med3_f32 v6, v6, s0, v1
	v_mov_b32_e32 v136, v5
	v_cvt_pk_fp8_f32 v136, v4, v6
	s_waitcnt vmcnt(29)
	v_mul_f32_e32 v14, 0x43800000, v102
	s_waitcnt vmcnt(28)
	v_mul_f32_e32 v4, 0x43800000, v90
	v_med3_f32 v6, v14, s0, v1
	v_med3_f32 v4, v4, s0, v1
	v_cvt_pk_fp8_f32 v136, v6, v4 op_sel:[0,0,1]
	s_waitcnt vmcnt(27)
	v_mul_f32_e32 v4, 0x43800000, v106
	s_waitcnt vmcnt(26)
	v_mul_f32_e32 v6, 0x43800000, v114
	v_med3_f32 v4, v4, s0, v1
	v_med3_f32 v6, v6, s0, v1
	v_mov_b32_e32 v137, v5
	v_cvt_pk_fp8_f32 v137, v4, v6
	s_waitcnt vmcnt(25)
	v_mul_f32_e32 v14, 0x43800000, v130
	s_waitcnt vmcnt(24)
	v_mul_f32_e32 v4, 0x43800000, v122
	v_med3_f32 v6, v14, s0, v1
	v_med3_f32 v4, v4, s0, v1
	v_cvt_pk_fp8_f32 v137, v6, v4 op_sel:[0,0,1]
	v_mul_f32_e32 v4, 0x43800000, v7
	v_mul_f32_e32 v6, 0x43800000, v15
	v_med3_f32 v4, v4, s0, v1
	v_med3_f32 v6, v6, s0, v1
	v_mov_b32_e32 v138, v5
	v_cvt_pk_fp8_f32 v138, v4, v6
	v_mul_f32_e32 v7, 0x43800000, v31
	v_mul_f32_e32 v4, 0x43800000, v23
	v_med3_f32 v6, v7, s0, v1
	v_med3_f32 v4, v4, s0, v1
	v_cvt_pk_fp8_f32 v138, v6, v4 op_sel:[0,0,1]
	v_mul_f32_e32 v4, 0x43800000, v39
	v_mul_f32_e32 v6, 0x43800000, v51
	v_med3_f32 v4, v4, s0, v1
	v_med3_f32 v6, v6, s0, v1
	v_mov_b32_e32 v139, v5
	v_cvt_pk_fp8_f32 v139, v4, v6
	v_mul_f32_e32 v7, 0x43800000, v71
	v_mul_f32_e32 v4, 0x43800000, v59
	v_med3_f32 v6, v7, s0, v1
	v_med3_f32 v4, v4, s0, v1
	v_cvt_pk_fp8_f32 v139, v6, v4 op_sel:[0,0,1]
	v_mul_f32_e32 v4, 0x43800000, v75
	v_mul_f32_e32 v6, 0x43800000, v83
	v_med3_f32 v4, v4, s0, v1
	v_med3_f32 v6, v6, s0, v1
	v_mov_b32_e32 v140, v5
	v_cvt_pk_fp8_f32 v140, v4, v6
	v_mul_f32_e32 v7, 0x43800000, v103
	v_mul_f32_e32 v4, 0x43800000, v91
	v_med3_f32 v6, v7, s0, v1
	v_med3_f32 v4, v4, s0, v1
	v_cvt_pk_fp8_f32 v140, v6, v4 op_sel:[0,0,1]
	v_mul_f32_e32 v4, 0x43800000, v107
	v_mul_f32_e32 v6, 0x43800000, v115
	v_med3_f32 v4, v4, s0, v1
	v_med3_f32 v6, v6, s0, v1
	v_mov_b32_e32 v141, v5
	v_cvt_pk_fp8_f32 v141, v4, v6
	v_mul_f32_e32 v7, 0x43800000, v131
	v_mul_f32_e32 v4, 0x43800000, v123
	v_med3_f32 v6, v7, s0, v1
	v_med3_f32 v4, v4, s0, v1
	v_cvt_pk_fp8_f32 v141, v6, v4 op_sel:[0,0,1]
	v_mul_f32_e32 v4, 0x43800000, v8
	v_mul_f32_e32 v6, 0x43800000, v16
	v_med3_f32 v4, v4, s0, v1
	v_med3_f32 v6, v6, s0, v1
	v_mov_b32_e32 v142, v5
	v_cvt_pk_fp8_f32 v142, v4, v6
	v_mul_f32_e32 v7, 0x43800000, v32
	v_mul_f32_e32 v4, 0x43800000, v24
	v_med3_f32 v6, v7, s0, v1
	v_med3_f32 v4, v4, s0, v1
	v_cvt_pk_fp8_f32 v142, v6, v4 op_sel:[0,0,1]
	v_mul_f32_e32 v4, 0x43800000, v40
	v_mul_f32_e32 v6, 0x43800000, v52
	v_med3_f32 v4, v4, s0, v1
	v_med3_f32 v6, v6, s0, v1
	v_mov_b32_e32 v143, v5
	v_cvt_pk_fp8_f32 v143, v4, v6
	v_mul_f32_e32 v7, 0x43800000, v72
	v_mul_f32_e32 v4, 0x43800000, v60
	v_med3_f32 v6, v7, s0, v1
	v_med3_f32 v4, v4, s0, v1
	v_cvt_pk_fp8_f32 v143, v6, v4 op_sel:[0,0,1]
	v_mul_f32_e32 v4, 0x43800000, v76
	v_mul_f32_e32 v6, 0x43800000, v84
	v_med3_f32 v4, v4, s0, v1
	v_med3_f32 v6, v6, s0, v1
	v_mov_b32_e32 v144, v5
	v_cvt_pk_fp8_f32 v144, v4, v6
	v_mul_f32_e32 v7, 0x43800000, v104
	v_mul_f32_e32 v4, 0x43800000, v92
	v_med3_f32 v6, v7, s0, v1
	v_med3_f32 v4, v4, s0, v1
	v_cvt_pk_fp8_f32 v144, v6, v4 op_sel:[0,0,1]
	v_mul_f32_e32 v4, 0x43800000, v108
	v_mul_f32_e32 v6, 0x43800000, v116
	v_med3_f32 v4, v4, s0, v1
	v_med3_f32 v6, v6, s0, v1
	v_mov_b32_e32 v145, v5
	v_cvt_pk_fp8_f32 v145, v4, v6
	v_mul_f32_e32 v7, 0x43800000, v132
	v_mul_f32_e32 v4, 0x43800000, v124
	v_med3_f32 v6, v7, s0, v1
	v_med3_f32 v4, v4, s0, v1
	v_cvt_pk_fp8_f32 v145, v6, v4 op_sel:[0,0,1]
	v_mul_f32_e32 v4, 0x43800000, v9
	v_mul_f32_e32 v6, 0x43800000, v17
	v_med3_f32 v4, v4, s0, v1
	v_med3_f32 v8, v6, s0, v1
	v_mov_b32_e32 v6, v5
	v_cvt_pk_fp8_f32 v6, v4, v8
	v_mul_f32_e32 v7, 0x43800000, v33
	v_mul_f32_e32 v4, 0x43800000, v25
	v_med3_f32 v7, v7, s0, v1
	v_med3_f32 v4, v4, s0, v1
	v_cvt_pk_fp8_f32 v6, v7, v4 op_sel:[0,0,1]
	v_mul_f32_e32 v4, 0x43800000, v41
	v_mul_f32_e32 v7, 0x43800000, v53
	v_med3_f32 v4, v4, s0, v1
	v_med3_f32 v9, v7, s0, v1
	v_mov_b32_e32 v7, v5
	v_cvt_pk_fp8_f32 v7, v4, v9
	v_mul_f32_e32 v8, 0x43800000, v73
	v_mul_f32_e32 v4, 0x43800000, v61
	v_med3_f32 v8, v8, s0, v1
	v_med3_f32 v4, v4, s0, v1
	v_cvt_pk_fp8_f32 v7, v8, v4 op_sel:[0,0,1]
	v_mul_f32_e32 v4, 0x43800000, v77
	v_mul_f32_e32 v8, 0x43800000, v85
	v_med3_f32 v4, v4, s0, v1
	v_med3_f32 v14, v8, s0, v1
	v_mov_b32_e32 v8, v5
	v_cvt_pk_fp8_f32 v8, v4, v14
	v_mul_f32_e32 v9, 0x43800000, v105
	v_mul_f32_e32 v4, 0x43800000, v93
	v_med3_f32 v9, v9, s0, v1
	v_med3_f32 v4, v4, s0, v1
	v_cvt_pk_fp8_f32 v8, v9, v4 op_sel:[0,0,1]
	v_mul_f32_e32 v4, 0x43800000, v109
	v_mul_f32_e32 v9, 0x43800000, v117
	v_med3_f32 v4, v4, s0, v1
	v_med3_f32 v15, v9, s0, v1
	v_mov_b32_e32 v9, v5
	v_cvt_pk_fp8_f32 v9, v4, v15
	v_mul_f32_e32 v14, 0x43800000, v133
	v_mul_f32_e32 v4, 0x43800000, v125
	v_med3_f32 v14, v14, s0, v1
	v_med3_f32 v4, v4, s0, v1
	v_cvt_pk_fp8_f32 v9, v14, v4 op_sel:[0,0,1]
	ds_write_b128 v166, v[134:137] offset:34816
	ds_write_b128 v166, v[138:141] offset:35088
	ds_write_b128 v166, v[142:145] offset:35360
	ds_write_b128 v166, v[6:9] offset:35632
	s_waitcnt lgkmcnt(0)
	s_barrier
	s_mov_b32 s1, 0x1c00000
	v_add_co_u32_e32 v6, vcc, s1, v2
	s_mov_b32 s1, 0x1c04000
	s_nop 0
	v_addc_co_u32_e32 v7, vcc, 0, v3, vcc
	v_add_co_u32_e32 v14, vcc, s1, v2
	s_mov_b32 s1, 0x1c08000
	s_nop 0
	v_addc_co_u32_e32 v15, vcc, 0, v3, vcc
	v_add_co_u32_e32 v22, vcc, s1, v2
	s_mov_b32 s1, 0x1c0c000
	s_nop 0
	v_addc_co_u32_e32 v23, vcc, 0, v3, vcc
	v_add_co_u32_e32 v24, vcc, s1, v2
	s_mov_b32 s1, 0x1c10000
	s_nop 0
	v_addc_co_u32_e32 v25, vcc, 0, v3, vcc
	v_add_co_u32_e32 v38, vcc, s1, v2
	s_mov_b32 s1, 0x1c14000
	s_nop 0
	v_addc_co_u32_e32 v39, vcc, 0, v3, vcc
	v_add_co_u32_e32 v50, vcc, s1, v2
	s_mov_b32 s1, 0x1c18000
	s_nop 0
	v_addc_co_u32_e32 v51, vcc, 0, v3, vcc
	v_add_co_u32_e32 v58, vcc, s1, v2
	s_mov_b32 s1, 0x1c1c000
	s_nop 0
	v_addc_co_u32_e32 v59, vcc, 0, v3, vcc
	v_add_co_u32_e32 v60, vcc, s1, v2
	s_mov_b32 s1, 0x1c20000
	s_nop 0
	v_addc_co_u32_e32 v61, vcc, 0, v3, vcc
	v_add_co_u32_e32 v74, vcc, s1, v2
	s_mov_b32 s1, 0x1c24000
	s_nop 0
	v_addc_co_u32_e32 v75, vcc, 0, v3, vcc
	v_add_co_u32_e32 v82, vcc, s1, v2
	s_mov_b32 s1, 0x1c28000
	s_nop 0
	v_addc_co_u32_e32 v83, vcc, 0, v3, vcc
	v_add_co_u32_e32 v90, vcc, s1, v2
	s_mov_b32 s1, 0x1c2c000
	s_nop 0
	v_addc_co_u32_e32 v91, vcc, 0, v3, vcc
	v_add_co_u32_e32 v92, vcc, s1, v2
	s_mov_b32 s1, 0x1c30000
	s_nop 0
	v_addc_co_u32_e32 v93, vcc, 0, v3, vcc
	v_add_co_u32_e32 v106, vcc, s1, v2
	s_mov_b32 s1, 0x1c34000
	s_nop 0
	v_addc_co_u32_e32 v107, vcc, 0, v3, vcc
	v_add_co_u32_e32 v114, vcc, s1, v2
	s_mov_b32 s1, 0x1c38000
	s_nop 0
	v_addc_co_u32_e32 v115, vcc, 0, v3, vcc
	v_add_co_u32_e32 v122, vcc, s1, v2
	s_mov_b32 s1, 0x1c3c000
	s_nop 0
	v_addc_co_u32_e32 v123, vcc, 0, v3, vcc
	v_add_co_u32_e32 v2, vcc, s1, v2
	global_load_dwordx4 v[6:9], v[6:7], off sc0 nt
	s_nop 0
	global_load_dwordx4 v[14:17], v[14:15], off sc0 nt
	s_nop 0
	global_load_dwordx4 v[30:33], v[22:23], off sc0 nt
	s_nop 0
	global_load_dwordx4 v[22:25], v[24:25], off sc0 nt
	s_nop 0
	global_load_dwordx4 v[38:41], v[38:39], off sc0 nt
	s_nop 0
	global_load_dwordx4 v[50:53], v[50:51], off sc0 nt
	s_nop 0
	global_load_dwordx4 v[70:73], v[58:59], off sc0 nt
	s_nop 0
	global_load_dwordx4 v[58:61], v[60:61], off sc0 nt
	s_nop 0
	global_load_dwordx4 v[74:77], v[74:75], off sc0 nt
	s_nop 0
	global_load_dwordx4 v[82:85], v[82:83], off sc0 nt
	s_nop 0
	global_load_dwordx4 v[102:105], v[90:91], off sc0 nt
	s_nop 0
	global_load_dwordx4 v[90:93], v[92:93], off sc0 nt
	s_nop 0
	global_load_dwordx4 v[106:109], v[106:107], off sc0 nt
	s_nop 0
	global_load_dwordx4 v[114:117], v[114:115], off sc0 nt
	v_addc_co_u32_e32 v3, vcc, 0, v3, vcc
	global_load_dwordx4 v[130:133], v[122:123], off sc0 nt
	s_nop 0
	global_load_dwordx4 v[122:125], v[2:3], off sc0 nt
	ds_read_b128 v[134:137], v154 offset:34816
	ds_read_b128 v[138:141], v156 offset:34816
	ds_read_b128 v[142:145], v158 offset:34816
	ds_read_b128 v[146:149], v162 offset:34816
	s_waitcnt lgkmcnt(3)
	global_store_dwordx4 v[150:151], v[134:137], off offset:1280 nt
	s_waitcnt lgkmcnt(2)
	global_store_dwordx4 v[152:153], v[138:141], off offset:1280 nt
	s_waitcnt lgkmcnt(1)
	global_store_dwordx4 v[160:161], v[142:145], off offset:1280 nt
	s_waitcnt lgkmcnt(0)
	global_store_dwordx4 v[164:165], v[146:149], off offset:1280 nt
	s_waitcnt vmcnt(39)
	v_mul_f32_e32 v2, 0x43800000, v10
	s_waitcnt vmcnt(38)
	v_mul_f32_e32 v3, 0x43800000, v18
	v_med3_f32 v2, v2, s0, v1
	v_med3_f32 v3, v3, s0, v1
	v_mov_b32_e32 v134, v5
	v_cvt_pk_fp8_f32 v134, v2, v3
	s_waitcnt vmcnt(37)
	v_mul_f32_e32 v4, 0x43800000, v34
	s_waitcnt vmcnt(36)
	v_mul_f32_e32 v2, 0x43800000, v26
	v_med3_f32 v3, v4, s0, v1
	v_med3_f32 v2, v2, s0, v1
	v_cvt_pk_fp8_f32 v134, v3, v2 op_sel:[0,0,1]
	s_waitcnt vmcnt(35)
	v_mul_f32_e32 v2, 0x43800000, v42
	s_waitcnt vmcnt(34)
	v_mul_f32_e32 v3, 0x43800000, v46
	v_med3_f32 v2, v2, s0, v1
	v_med3_f32 v3, v3, s0, v1
	v_mov_b32_e32 v135, v5
	v_cvt_pk_fp8_f32 v135, v2, v3
	s_waitcnt vmcnt(33)
	v_mul_f32_e32 v4, 0x43800000, v62
	s_waitcnt vmcnt(32)
	v_mul_f32_e32 v2, 0x43800000, v54
	v_med3_f32 v3, v4, s0, v1
	v_med3_f32 v2, v2, s0, v1
	v_cvt_pk_fp8_f32 v135, v3, v2 op_sel:[0,0,1]
	s_waitcnt vmcnt(31)
	v_mul_f32_e32 v2, 0x43800000, v66
	s_waitcnt vmcnt(30)
	v_mul_f32_e32 v3, 0x43800000, v78
	v_med3_f32 v2, v2, s0, v1
	v_med3_f32 v3, v3, s0, v1
	v_mov_b32_e32 v136, v5
	v_cvt_pk_fp8_f32 v136, v2, v3
	s_waitcnt vmcnt(29)
	v_mul_f32_e32 v4, 0x43800000, v94
	s_waitcnt vmcnt(28)
	v_mul_f32_e32 v2, 0x43800000, v86
	v_med3_f32 v3, v4, s0, v1
	v_med3_f32 v2, v2, s0, v1
	v_cvt_pk_fp8_f32 v136, v3, v2 op_sel:[0,0,1]
	s_waitcnt vmcnt(27)
	v_mul_f32_e32 v2, 0x43800000, v98
	s_waitcnt vmcnt(26)
	v_mul_f32_e32 v3, 0x43800000, v110
	v_med3_f32 v2, v2, s0, v1
	v_med3_f32 v3, v3, s0, v1
	v_mov_b32_e32 v137, v5
	v_cvt_pk_fp8_f32 v137, v2, v3
	s_waitcnt vmcnt(25)
	v_mul_f32_e32 v4, 0x43800000, v126
	s_waitcnt vmcnt(24)
	v_mul_f32_e32 v2, 0x43800000, v118
	v_med3_f32 v3, v4, s0, v1
	v_med3_f32 v2, v2, s0, v1
	v_cvt_pk_fp8_f32 v137, v3, v2 op_sel:[0,0,1]
	v_mul_f32_e32 v2, 0x43800000, v11
	v_mul_f32_e32 v3, 0x43800000, v19
	v_med3_f32 v2, v2, s0, v1
	v_med3_f32 v3, v3, s0, v1
	v_mov_b32_e32 v138, v5
	v_cvt_pk_fp8_f32 v138, v2, v3
	v_mul_f32_e32 v4, 0x43800000, v35
	v_mul_f32_e32 v2, 0x43800000, v27
	v_med3_f32 v3, v4, s0, v1
	v_med3_f32 v2, v2, s0, v1
	v_cvt_pk_fp8_f32 v138, v3, v2 op_sel:[0,0,1]
	v_mul_f32_e32 v2, 0x43800000, v43
	v_mul_f32_e32 v3, 0x43800000, v47
	v_med3_f32 v2, v2, s0, v1
	v_med3_f32 v3, v3, s0, v1
	v_mov_b32_e32 v139, v5
	v_cvt_pk_fp8_f32 v139, v2, v3
	v_mul_f32_e32 v4, 0x43800000, v63
	v_mul_f32_e32 v2, 0x43800000, v55
	v_med3_f32 v3, v4, s0, v1
	v_med3_f32 v2, v2, s0, v1
	v_cvt_pk_fp8_f32 v139, v3, v2 op_sel:[0,0,1]
	v_mul_f32_e32 v2, 0x43800000, v67
	v_mul_f32_e32 v3, 0x43800000, v79
	v_med3_f32 v2, v2, s0, v1
	v_med3_f32 v3, v3, s0, v1
	v_mov_b32_e32 v140, v5
	v_cvt_pk_fp8_f32 v140, v2, v3
	v_mul_f32_e32 v4, 0x43800000, v95
	v_mul_f32_e32 v2, 0x43800000, v87
	v_med3_f32 v3, v4, s0, v1
	v_med3_f32 v2, v2, s0, v1
	v_cvt_pk_fp8_f32 v140, v3, v2 op_sel:[0,0,1]
	v_mul_f32_e32 v2, 0x43800000, v99
	v_mul_f32_e32 v3, 0x43800000, v111
	v_med3_f32 v2, v2, s0, v1
	v_med3_f32 v3, v3, s0, v1
	v_mov_b32_e32 v141, v5
	v_cvt_pk_fp8_f32 v141, v2, v3
	v_mul_f32_e32 v4, 0x43800000, v127
	v_mul_f32_e32 v2, 0x43800000, v119
	v_med3_f32 v3, v4, s0, v1
	v_med3_f32 v2, v2, s0, v1
	v_cvt_pk_fp8_f32 v141, v3, v2 op_sel:[0,0,1]
	v_mul_f32_e32 v2, 0x43800000, v12
	v_mul_f32_e32 v3, 0x43800000, v20
	v_med3_f32 v2, v2, s0, v1
	v_med3_f32 v3, v3, s0, v1
	v_mov_b32_e32 v142, v5
	v_cvt_pk_fp8_f32 v142, v2, v3
	v_mul_f32_e32 v4, 0x43800000, v36
	v_mul_f32_e32 v2, 0x43800000, v28
	v_med3_f32 v3, v4, s0, v1
	v_med3_f32 v2, v2, s0, v1
	v_cvt_pk_fp8_f32 v142, v3, v2 op_sel:[0,0,1]
	v_mul_f32_e32 v2, 0x43800000, v44
	v_mul_f32_e32 v3, 0x43800000, v48
	v_med3_f32 v2, v2, s0, v1
	v_med3_f32 v3, v3, s0, v1
	v_mov_b32_e32 v143, v5
	v_cvt_pk_fp8_f32 v143, v2, v3
	v_mul_f32_e32 v4, 0x43800000, v64
	v_mul_f32_e32 v2, 0x43800000, v56
	v_med3_f32 v3, v4, s0, v1
	v_med3_f32 v2, v2, s0, v1
	v_cvt_pk_fp8_f32 v143, v3, v2 op_sel:[0,0,1]
	v_mul_f32_e32 v2, 0x43800000, v68
	v_mul_f32_e32 v3, 0x43800000, v80
	v_med3_f32 v2, v2, s0, v1
	v_med3_f32 v3, v3, s0, v1
	v_mov_b32_e32 v144, v5
	v_cvt_pk_fp8_f32 v144, v2, v3
	v_mul_f32_e32 v4, 0x43800000, v96
	v_mul_f32_e32 v2, 0x43800000, v88
	v_med3_f32 v3, v4, s0, v1
	v_med3_f32 v2, v2, s0, v1
	v_cvt_pk_fp8_f32 v144, v3, v2 op_sel:[0,0,1]
	v_mul_f32_e32 v2, 0x43800000, v100
	v_mul_f32_e32 v3, 0x43800000, v112
	v_med3_f32 v2, v2, s0, v1
	v_med3_f32 v3, v3, s0, v1
	v_mov_b32_e32 v145, v5
	v_cvt_pk_fp8_f32 v145, v2, v3
	v_mul_f32_e32 v4, 0x43800000, v128
	v_mul_f32_e32 v2, 0x43800000, v120
	v_med3_f32 v3, v4, s0, v1
	v_med3_f32 v2, v2, s0, v1
	v_cvt_pk_fp8_f32 v145, v3, v2 op_sel:[0,0,1]
	v_mul_f32_e32 v2, 0x43800000, v13
	v_mul_f32_e32 v3, 0x43800000, v21
	v_med3_f32 v2, v2, s0, v1
	v_med3_f32 v3, v3, s0, v1
	v_mov_b32_e32 v10, v5
	v_cvt_pk_fp8_f32 v10, v2, v3
	v_mul_f32_e32 v4, 0x43800000, v37
	v_mul_f32_e32 v2, 0x43800000, v29
	v_med3_f32 v3, v4, s0, v1
	v_med3_f32 v2, v2, s0, v1
	v_cvt_pk_fp8_f32 v10, v3, v2 op_sel:[0,0,1]
	v_mul_f32_e32 v2, 0x43800000, v45
	v_mul_f32_e32 v3, 0x43800000, v49
	v_med3_f32 v2, v2, s0, v1
	v_med3_f32 v3, v3, s0, v1
	v_mov_b32_e32 v11, v5
	v_cvt_pk_fp8_f32 v11, v2, v3
	v_mul_f32_e32 v4, 0x43800000, v65
	v_mul_f32_e32 v2, 0x43800000, v57
	v_med3_f32 v3, v4, s0, v1
	v_med3_f32 v2, v2, s0, v1
	v_cvt_pk_fp8_f32 v11, v3, v2 op_sel:[0,0,1]
	v_mul_f32_e32 v2, 0x43800000, v69
	v_mul_f32_e32 v3, 0x43800000, v81
	v_med3_f32 v2, v2, s0, v1
	v_med3_f32 v3, v3, s0, v1
	v_mov_b32_e32 v12, v5
	v_cvt_pk_fp8_f32 v12, v2, v3
	v_mul_f32_e32 v4, 0x43800000, v97
	v_mul_f32_e32 v2, 0x43800000, v89
	v_med3_f32 v3, v4, s0, v1
	v_med3_f32 v2, v2, s0, v1
	v_cvt_pk_fp8_f32 v12, v3, v2 op_sel:[0,0,1]
	v_mul_f32_e32 v2, 0x43800000, v101
	v_mul_f32_e32 v3, 0x43800000, v113
	v_med3_f32 v2, v2, s0, v1
	v_med3_f32 v3, v3, s0, v1
	v_mov_b32_e32 v13, v5
	v_cvt_pk_fp8_f32 v13, v2, v3
	v_mul_f32_e32 v4, 0x43800000, v129
	v_mul_f32_e32 v2, 0x43800000, v121
	v_med3_f32 v3, v4, s0, v1
	v_med3_f32 v2, v2, s0, v1
	v_cvt_pk_fp8_f32 v13, v3, v2 op_sel:[0,0,1]
	ds_write_b128 v166, v[134:137]
	ds_write_b128 v166, v[138:141] offset:272
	ds_write_b128 v166, v[142:145] offset:544
	ds_write_b128 v166, v[10:13] offset:816
	s_waitcnt lgkmcnt(0)
	s_barrier
	ds_read_b128 v[10:13], v154
	ds_read_b128 v[18:21], v156
	ds_read_b128 v[26:29], v158
	ds_read_b128 v[34:37], v162
	s_waitcnt lgkmcnt(3)
	global_store_dwordx4 v[150:151], v[10:13], off offset:1536 nt
	s_waitcnt lgkmcnt(2)
	global_store_dwordx4 v[152:153], v[18:21], off offset:1536 nt
	s_waitcnt lgkmcnt(1)
	global_store_dwordx4 v[160:161], v[26:29], off offset:1536 nt
	s_waitcnt lgkmcnt(0)
	global_store_dwordx4 v[164:165], v[34:37], off offset:1536 nt
	s_waitcnt vmcnt(23)
	v_mul_f32_e32 v2, 0x43800000, v6
	s_waitcnt vmcnt(22)
	v_mul_f32_e32 v3, 0x43800000, v14
	v_med3_f32 v2, v2, s0, v1
	v_med3_f32 v3, v3, s0, v1
	v_mov_b32_e32 v10, v5
	v_cvt_pk_fp8_f32 v10, v2, v3
	s_waitcnt vmcnt(21)
	v_mul_f32_e32 v4, 0x43800000, v30
	s_waitcnt vmcnt(20)
	v_mul_f32_e32 v2, 0x43800000, v22
	v_med3_f32 v3, v4, s0, v1
	v_med3_f32 v2, v2, s0, v1
	v_cvt_pk_fp8_f32 v10, v3, v2 op_sel:[0,0,1]
	s_waitcnt vmcnt(19)
	v_mul_f32_e32 v2, 0x43800000, v38
	s_waitcnt vmcnt(18)
	v_mul_f32_e32 v3, 0x43800000, v50
	v_med3_f32 v2, v2, s0, v1
	v_med3_f32 v3, v3, s0, v1
	v_mov_b32_e32 v11, v5
	v_cvt_pk_fp8_f32 v11, v2, v3
	s_waitcnt vmcnt(17)
	v_mul_f32_e32 v4, 0x43800000, v70
	s_waitcnt vmcnt(16)
	v_mul_f32_e32 v2, 0x43800000, v58
	v_med3_f32 v3, v4, s0, v1
	v_med3_f32 v2, v2, s0, v1
	v_cvt_pk_fp8_f32 v11, v3, v2 op_sel:[0,0,1]
	s_waitcnt vmcnt(15)
	v_mul_f32_e32 v2, 0x43800000, v74
	s_waitcnt vmcnt(14)
	v_mul_f32_e32 v3, 0x43800000, v82
	v_med3_f32 v2, v2, s0, v1
	v_med3_f32 v3, v3, s0, v1
	v_mov_b32_e32 v12, v5
	v_cvt_pk_fp8_f32 v12, v2, v3
	s_waitcnt vmcnt(13)
	v_mul_f32_e32 v4, 0x43800000, v102
	s_waitcnt vmcnt(12)
	v_mul_f32_e32 v2, 0x43800000, v90
	v_med3_f32 v3, v4, s0, v1
	v_med3_f32 v2, v2, s0, v1
	v_cvt_pk_fp8_f32 v12, v3, v2 op_sel:[0,0,1]
	s_waitcnt vmcnt(11)
	v_mul_f32_e32 v2, 0x43800000, v106
	s_waitcnt vmcnt(10)
	v_mul_f32_e32 v3, 0x43800000, v114
	v_med3_f32 v2, v2, s0, v1
	v_med3_f32 v3, v3, s0, v1
	v_mov_b32_e32 v13, v5
	v_cvt_pk_fp8_f32 v13, v2, v3
	s_waitcnt vmcnt(9)
	v_mul_f32_e32 v4, 0x43800000, v130
	s_waitcnt vmcnt(8)
	v_mul_f32_e32 v2, 0x43800000, v122
	v_med3_f32 v3, v4, s0, v1
	v_med3_f32 v2, v2, s0, v1
	v_cvt_pk_fp8_f32 v13, v3, v2 op_sel:[0,0,1]
	v_mul_f32_e32 v2, 0x43800000, v7
	v_mul_f32_e32 v3, 0x43800000, v15
	v_med3_f32 v2, v2, s0, v1
	v_med3_f32 v3, v3, s0, v1
	v_mov_b32_e32 v18, v5
	v_cvt_pk_fp8_f32 v18, v2, v3
	v_mul_f32_e32 v4, 0x43800000, v31
	v_mul_f32_e32 v2, 0x43800000, v23
	v_med3_f32 v3, v4, s0, v1
	v_med3_f32 v2, v2, s0, v1
	v_cvt_pk_fp8_f32 v18, v3, v2 op_sel:[0,0,1]
	v_mul_f32_e32 v2, 0x43800000, v39
	v_mul_f32_e32 v3, 0x43800000, v51
	v_med3_f32 v2, v2, s0, v1
	v_med3_f32 v3, v3, s0, v1
	v_mov_b32_e32 v19, v5
	v_cvt_pk_fp8_f32 v19, v2, v3
	v_mul_f32_e32 v4, 0x43800000, v71
	v_mul_f32_e32 v2, 0x43800000, v59
	v_med3_f32 v3, v4, s0, v1
	v_med3_f32 v2, v2, s0, v1
	v_cvt_pk_fp8_f32 v19, v3, v2 op_sel:[0,0,1]
	v_mul_f32_e32 v2, 0x43800000, v75
	v_mul_f32_e32 v3, 0x43800000, v83
	v_med3_f32 v2, v2, s0, v1
	v_med3_f32 v3, v3, s0, v1
	v_mov_b32_e32 v20, v5
	v_cvt_pk_fp8_f32 v20, v2, v3
	v_mul_f32_e32 v4, 0x43800000, v103
	v_mul_f32_e32 v2, 0x43800000, v91
	v_med3_f32 v3, v4, s0, v1
	v_med3_f32 v2, v2, s0, v1
	v_cvt_pk_fp8_f32 v20, v3, v2 op_sel:[0,0,1]
	v_mul_f32_e32 v2, 0x43800000, v107
	v_mul_f32_e32 v3, 0x43800000, v115
	v_med3_f32 v2, v2, s0, v1
	v_med3_f32 v3, v3, s0, v1
	v_mov_b32_e32 v21, v5
	v_cvt_pk_fp8_f32 v21, v2, v3
	v_mul_f32_e32 v4, 0x43800000, v131
	v_mul_f32_e32 v2, 0x43800000, v123
	v_med3_f32 v3, v4, s0, v1
	v_med3_f32 v2, v2, s0, v1
	v_cvt_pk_fp8_f32 v21, v3, v2 op_sel:[0,0,1]
	v_mul_f32_e32 v2, 0x43800000, v8
	v_mul_f32_e32 v3, 0x43800000, v16
	v_med3_f32 v2, v2, s0, v1
	v_med3_f32 v3, v3, s0, v1
	v_mov_b32_e32 v26, v5
	v_cvt_pk_fp8_f32 v26, v2, v3
	v_mul_f32_e32 v4, 0x43800000, v32
	v_mul_f32_e32 v2, 0x43800000, v24
	v_med3_f32 v3, v4, s0, v1
	v_med3_f32 v2, v2, s0, v1
	v_cvt_pk_fp8_f32 v26, v3, v2 op_sel:[0,0,1]
	v_mul_f32_e32 v2, 0x43800000, v40
	v_mul_f32_e32 v3, 0x43800000, v52
	v_med3_f32 v2, v2, s0, v1
	v_med3_f32 v3, v3, s0, v1
	v_mov_b32_e32 v27, v5
	v_cvt_pk_fp8_f32 v27, v2, v3
	v_mul_f32_e32 v4, 0x43800000, v72
	v_mul_f32_e32 v2, 0x43800000, v60
	v_med3_f32 v3, v4, s0, v1
	v_med3_f32 v2, v2, s0, v1
	v_cvt_pk_fp8_f32 v27, v3, v2 op_sel:[0,0,1]
	v_mul_f32_e32 v2, 0x43800000, v76
	v_mul_f32_e32 v3, 0x43800000, v84
	v_med3_f32 v2, v2, s0, v1
	v_med3_f32 v3, v3, s0, v1
	v_mov_b32_e32 v28, v5
	v_cvt_pk_fp8_f32 v28, v2, v3
	v_mul_f32_e32 v4, 0x43800000, v104
	v_mul_f32_e32 v2, 0x43800000, v92
	v_med3_f32 v3, v4, s0, v1
	v_med3_f32 v2, v2, s0, v1
	v_cvt_pk_fp8_f32 v28, v3, v2 op_sel:[0,0,1]
	v_mul_f32_e32 v2, 0x43800000, v108
	v_mul_f32_e32 v3, 0x43800000, v116
	v_med3_f32 v2, v2, s0, v1
	v_med3_f32 v3, v3, s0, v1
	v_mov_b32_e32 v29, v5
	v_cvt_pk_fp8_f32 v29, v2, v3
	v_mul_f32_e32 v4, 0x43800000, v132
	v_mul_f32_e32 v2, 0x43800000, v124
	v_med3_f32 v3, v4, s0, v1
	v_med3_f32 v2, v2, s0, v1
	v_cvt_pk_fp8_f32 v29, v3, v2 op_sel:[0,0,1]
	v_mul_f32_e32 v2, 0x43800000, v9
	v_mul_f32_e32 v3, 0x43800000, v17
	v_med3_f32 v6, v2, s0, v1
	v_med3_f32 v3, v3, s0, v1
	v_mov_b32_e32 v2, v5
	v_cvt_pk_fp8_f32 v2, v6, v3
	v_mul_f32_e32 v4, 0x43800000, v33
	v_mul_f32_e32 v3, 0x43800000, v25
	v_med3_f32 v4, v4, s0, v1
	v_med3_f32 v3, v3, s0, v1
	v_cvt_pk_fp8_f32 v2, v4, v3 op_sel:[0,0,1]
	v_mul_f32_e32 v3, 0x43800000, v41
	v_mul_f32_e32 v4, 0x43800000, v53
	v_med3_f32 v7, v3, s0, v1
	v_med3_f32 v4, v4, s0, v1
	v_mov_b32_e32 v3, v5
	v_cvt_pk_fp8_f32 v3, v7, v4
	v_mul_f32_e32 v6, 0x43800000, v73
	v_mul_f32_e32 v4, 0x43800000, v61
	v_med3_f32 v6, v6, s0, v1
	v_med3_f32 v4, v4, s0, v1
	v_cvt_pk_fp8_f32 v3, v6, v4 op_sel:[0,0,1]
	v_mul_f32_e32 v4, 0x43800000, v77
	v_mul_f32_e32 v6, 0x43800000, v85
	v_med3_f32 v8, v4, s0, v1
	v_med3_f32 v6, v6, s0, v1
	v_mov_b32_e32 v4, v5
	v_cvt_pk_fp8_f32 v4, v8, v6
	v_mul_f32_e32 v7, 0x43800000, v105
	v_mul_f32_e32 v6, 0x43800000, v93
	v_med3_f32 v7, v7, s0, v1
	v_med3_f32 v6, v6, s0, v1
	v_cvt_pk_fp8_f32 v4, v7, v6 op_sel:[0,0,1]
	v_mul_f32_e32 v6, 0x43800000, v109
	v_mul_f32_e32 v7, 0x43800000, v117
	v_med3_f32 v6, v6, s0, v1
	v_med3_f32 v7, v7, s0, v1
	v_cvt_pk_fp8_f32 v5, v6, v7
	v_mul_f32_e32 v8, 0x43800000, v133
	v_mul_f32_e32 v6, 0x43800000, v125
	v_med3_f32 v7, v8, s0, v1
	v_med3_f32 v1, v6, s0, v1
	v_cvt_pk_fp8_f32 v5, v7, v1 op_sel:[0,0,1]
	ds_write_b128 v166, v[10:13] offset:34816
	ds_write_b128 v166, v[18:21] offset:35088
	ds_write_b128 v166, v[26:29] offset:35360
	ds_write_b128 v166, v[2:5] offset:35632
	s_waitcnt lgkmcnt(0)
	s_barrier
	ds_read_b128 v[2:5], v154 offset:34816
	ds_read_b128 v[6:9], v156 offset:34816
	ds_read_b128 v[10:13], v158 offset:34816
	ds_read_b128 v[14:17], v162 offset:34816
	s_waitcnt lgkmcnt(3)
	global_store_dwordx4 v[150:151], v[2:5], off offset:1792 nt
	s_waitcnt lgkmcnt(2)
	global_store_dwordx4 v[152:153], v[6:9], off offset:1792 nt
	s_waitcnt lgkmcnt(1)
	global_store_dwordx4 v[160:161], v[10:13], off offset:1792 nt
	s_waitcnt lgkmcnt(0)
	global_store_dwordx4 v[164:165], v[14:17], off offset:1792 nt
	s_barrier

.LBB0_689:
	s_add_i32 s2, s1, 0x200
	s_ashr_i32 s8, s2, 5
	s_ashr_i32 s9, s8, 31
	v_readlane_b32 s20, v254, 4
	s_and_b32 s2, s1, 31
	s_lshl_b64 s[10:11], s[8:9], 25
	v_readlane_b32 s22, v254, 6
	v_readlane_b32 s23, v254, 7
	s_add_u32 s10, s22, s10
	s_addc_u32 s11, s23, s11
	s_lshl_b32 s12, s1, 6
	s_lshl_b32 s1, s1, 11
	s_and_b32 s12, s12, 0x780
	s_and_b32 s1, s1, 0x800
	s_or_b32 s1, s12, s1
	s_lshl_b32 s1, s1, 2
	s_add_u32 s10, s10, s1
	s_addc_u32 s11, s11, 0
	s_lshl_b32 s1, s2, 18
	s_lshl_b64 s[8:9], s[8:9], 23
	s_add_u32 s2, s70, s8
	v_mov_b32_e32 v130, v0
	s_addc_u32 s9, s71, s9
	s_add_u32 s8, s2, s1
	v_readfirstlane_b32 s7, v130
	s_addc_u32 s9, s9, 0
	s_ashr_i32 s1, s7, 1
	v_lshrrev_b32_e32 v1, 1, v130
	s_andn2_b32 s1, s1, 31
	v_and_b32_e32 v1, 16, v1
	v_or_b32_e32 v2, s1, v1
	v_ashrrev_i32_e32 v3, 31, v2
	v_lshlrev_b32_e32 v4, 2, v130
	v_lshlrev_b64 v[2:3], 14, v[2:3]
	v_and_b32_e32 v131, 0x7c, v4
	v_lshl_add_u64 v[2:3], s[10:11], 0, v[2:3]
	v_lshlrev_b32_e32 v162, 2, v131
	v_lshl_add_u64 v[164:165], v[2:3], 0, v[162:163]
	s_movk_i32 s2, 0x4000
	v_add_co_u32_e32 v2, vcc, s2, v164
	s_mov_b32 s2, 0x8000
	s_nop 0
	v_addc_co_u32_e32 v3, vcc, 0, v165, vcc
	global_load_dwordx4 v[82:85], v[164:165], off sc0 nt
	global_load_dwordx4 v[90:93], v[2:3], off sc0 nt
	v_add_co_u32_e32 v2, vcc, s2, v164
	s_mov_b32 s2, 0xc000
	s_nop 0
	v_addc_co_u32_e32 v3, vcc, 0, v165, vcc
	v_add_co_u32_e32 v4, vcc, s2, v164
	s_mov_b32 s2, 0x10000
	s_nop 0
	v_addc_co_u32_e32 v5, vcc, 0, v165, vcc
	global_load_dwordx4 v[114:117], v[2:3], off sc0 nt
	global_load_dwordx4 v[118:121], v[4:5], off sc0 nt
	v_add_co_u32_e32 v2, vcc, s2, v164
	s_mov_b32 s2, 0x14000
	s_nop 0
	v_addc_co_u32_e32 v3, vcc, 0, v165, vcc
	v_add_co_u32_e32 v4, vcc, s2, v164
	s_mov_b32 s2, 0x18000
	s_nop 0
	v_addc_co_u32_e32 v5, vcc, 0, v165, vcc
	global_load_dwordx4 v[50:53], v[2:3], off sc0 nt
	global_load_dwordx4 v[58:61], v[4:5], off sc0 nt
	v_add_co_u32_e32 v2, vcc, s2, v164
	s_mov_b32 s2, 0x1c000
	s_nop 0
	v_addc_co_u32_e32 v3, vcc, 0, v165, vcc
	v_add_co_u32_e32 v4, vcc, s2, v164
	s_mov_b32 s2, 0x20000
	s_nop 0
	v_addc_co_u32_e32 v5, vcc, 0, v165, vcc
	global_load_dwordx4 v[86:89], v[2:3], off sc0 nt
	global_load_dwordx4 v[94:97], v[4:5], off sc0 nt
	v_add_co_u32_e32 v2, vcc, s2, v164
	s_mov_b32 s2, 0x24000
	s_nop 0
	v_addc_co_u32_e32 v3, vcc, 0, v165, vcc
	v_add_co_u32_e32 v4, vcc, s2, v164
	s_mov_b32 s2, 0x28000
	s_nop 0
	v_addc_co_u32_e32 v5, vcc, 0, v165, vcc
	global_load_dwordx4 v[18:21], v[2:3], off sc0 nt
	global_load_dwordx4 v[26:29], v[4:5], off sc0 nt
	v_add_co_u32_e32 v2, vcc, s2, v164
	s_mov_b32 s2, 0x2c000
	s_nop 0
	v_addc_co_u32_e32 v3, vcc, 0, v165, vcc
	v_add_co_u32_e32 v4, vcc, s2, v164
	s_mov_b32 s2, 0x30000
	s_nop 0
	v_addc_co_u32_e32 v5, vcc, 0, v165, vcc
	global_load_dwordx4 v[54:57], v[2:3], off sc0 nt
	global_load_dwordx4 v[62:65], v[4:5], off sc0 nt
	v_add_co_u32_e32 v2, vcc, s2, v164
	s_mov_b32 s2, 0x34000
	s_nop 0
	v_addc_co_u32_e32 v3, vcc, 0, v165, vcc
	v_add_co_u32_e32 v6, vcc, s2, v164
	s_mov_b32 s2, 0x38000
	s_nop 0
	v_addc_co_u32_e32 v7, vcc, 0, v165, vcc
	v_add_co_u32_e32 v10, vcc, s2, v164
	s_mov_b32 s2, 0x3c000
	s_nop 0
	v_addc_co_u32_e32 v11, vcc, 0, v165, vcc
	v_add_co_u32_e32 v12, vcc, s2, v164
	s_mov_b32 s2, 0x400000
	s_nop 0
	v_addc_co_u32_e32 v13, vcc, 0, v165, vcc
	global_load_dwordx4 v[2:5], v[2:3], off sc0 nt
	s_nop 0
	global_load_dwordx4 v[6:9], v[6:7], off sc0 nt
	s_nop 0
	global_load_dwordx4 v[22:25], v[10:11], off sc0 nt
	global_load_dwordx4 v[30:33], v[12:13], off sc0 nt
	v_add_co_u32_e32 v10, vcc, s2, v164
	s_mov_b32 s2, 0x404000
	s_nop 0
	v_addc_co_u32_e32 v11, vcc, 0, v165, vcc
	v_add_co_u32_e32 v12, vcc, s2, v164
	s_mov_b32 s2, 0x408000
	s_nop 0
	v_addc_co_u32_e32 v13, vcc, 0, v165, vcc
	global_load_dwordx4 v[98:101], v[10:11], off sc0 nt
	global_load_dwordx4 v[106:109], v[12:13], off sc0 nt
	v_add_co_u32_e32 v10, vcc, s2, v164
	s_mov_b32 s2, 0x40c000
	s_nop 0
	v_addc_co_u32_e32 v11, vcc, 0, v165, vcc
	v_add_co_u32_e32 v12, vcc, s2, v164
	s_mov_b32 s2, 0x410000
	s_nop 0
	v_addc_co_u32_e32 v13, vcc, 0, v165, vcc
	global_load_dwordx4 v[122:125], v[10:11], off sc0 nt
	global_load_dwordx4 v[126:129], v[12:13], off sc0 nt
	v_add_co_u32_e32 v10, vcc, s2, v164
	s_mov_b32 s2, 0x414000
	s_nop 0
	v_addc_co_u32_e32 v11, vcc, 0, v165, vcc
	v_add_co_u32_e32 v12, vcc, s2, v164
	s_mov_b32 s2, 0x418000
	s_nop 0
	v_addc_co_u32_e32 v13, vcc, 0, v165, vcc
	global_load_dwordx4 v[66:69], v[10:11], off sc0 nt
	global_load_dwordx4 v[74:77], v[12:13], off sc0 nt
	v_add_co_u32_e32 v10, vcc, s2, v164
	s_mov_b32 s2, 0x41c000
	s_nop 0
	v_addc_co_u32_e32 v11, vcc, 0, v165, vcc
	v_add_co_u32_e32 v12, vcc, s2, v164
	s_mov_b32 s2, 0x420000
	s_nop 0
	v_addc_co_u32_e32 v13, vcc, 0, v165, vcc
	global_load_dwordx4 v[102:105], v[10:11], off sc0 nt
	global_load_dwordx4 v[110:113], v[12:13], off sc0 nt
	v_add_co_u32_e32 v10, vcc, s2, v164
	s_mov_b32 s2, 0x424000
	s_nop 0
	v_addc_co_u32_e32 v11, vcc, 0, v165, vcc
	v_add_co_u32_e32 v12, vcc, s2, v164
	s_mov_b32 s2, 0x428000
	s_nop 0
	v_addc_co_u32_e32 v13, vcc, 0, v165, vcc
	global_load_dwordx4 v[34:37], v[10:11], off sc0 nt
	global_load_dwordx4 v[42:45], v[12:13], off sc0 nt
	v_add_co_u32_e32 v10, vcc, s2, v164
	s_mov_b32 s2, 0x42c000
	s_nop 0
	v_addc_co_u32_e32 v11, vcc, 0, v165, vcc
	v_add_co_u32_e32 v12, vcc, s2, v164
	s_mov_b32 s2, 0x430000
	s_nop 0
	v_addc_co_u32_e32 v13, vcc, 0, v165, vcc
	global_load_dwordx4 v[70:73], v[10:11], off sc0 nt
	global_load_dwordx4 v[78:81], v[12:13], off sc0 nt
	v_add_co_u32_e32 v10, vcc, s2, v164
	s_mov_b32 s2, 0x434000
	s_nop 0
	v_addc_co_u32_e32 v11, vcc, 0, v165, vcc
	v_add_co_u32_e32 v14, vcc, s2, v164
	s_mov_b32 s2, 0x438000
	s_nop 0
	v_addc_co_u32_e32 v15, vcc, 0, v165, vcc
	s_waitcnt vmcnt(50)
	v_add_co_u32_e32 v38, vcc, s2, v164
	s_mov_b32 s2, 0x43c000
	s_nop 0
	v_addc_co_u32_e32 v39, vcc, 0, v165, vcc
	s_waitcnt vmcnt(47)
	v_add_co_u32_e32 v46, vcc, s2, v164
	global_load_dwordx4 v[10:13], v[10:11], off sc0 nt
	s_nop 0
	global_load_dwordx4 v[14:17], v[14:15], off sc0 nt
	v_addc_co_u32_e32 v47, vcc, 0, v165, vcc
	global_load_dwordx4 v[38:41], v[38:39], off sc0 nt
	s_nop 0
	global_load_dwordx4 v[46:49], v[46:47], off sc0 nt
	v_readlane_b32 s21, v254, 5
	v_readlane_b32 s24, v254, 8
	v_readlane_b32 s25, v254, 9
	v_readlane_b32 s26, v254, 10
	v_readlane_b32 s27, v254, 11
	s_waitcnt vmcnt(31)
	v_mul_f32_e32 v82, 0x43800000, v82
	s_waitcnt vmcnt(30)
	v_mul_f32_e32 v90, 0x43800000, v90
	s_waitcnt vmcnt(27)
	v_mul_f32_e32 v50, 0x43800000, v50
	s_waitcnt vmcnt(26)
	v_mul_f32_e32 v58, 0x43800000, v58
	s_waitcnt vmcnt(23)
	v_mul_f32_e32 v18, 0x43800000, v18
	s_waitcnt vmcnt(22)
	v_mul_f32_e32 v26, 0x43800000, v26
	s_waitcnt vmcnt(19)
	v_mul_f32_e32 v2, 0x43800000, v2
	s_waitcnt vmcnt(18)
	v_mul_f32_e32 v6, 0x43800000, v6
	v_med3_f32 v82, v82, s54, v192
	v_med3_f32 v90, v90, s54, v192
	v_mov_b32_e32 v132, v163
	v_med3_f32 v50, v50, s54, v192
	v_med3_f32 v58, v58, s54, v192
	v_mov_b32_e32 v133, v163
	v_med3_f32 v18, v18, s54, v192
	v_med3_f32 v26, v26, s54, v192
	v_mov_b32_e32 v134, v163
	v_med3_f32 v2, v2, s54, v192
	v_med3_f32 v6, v6, s54, v192
	v_mov_b32_e32 v135, v163
	v_cvt_pk_fp8_f32 v132, v82, v90
	v_cvt_pk_fp8_f32 v133, v50, v58
	v_cvt_pk_fp8_f32 v134, v18, v26
	v_cvt_pk_fp8_f32 v135, v2, v6
	v_mul_f32_e32 v114, 0x43800000, v114
	v_mul_f32_e32 v118, 0x43800000, v118
	v_mul_f32_e32 v82, 0x43800000, v86
	v_mul_f32_e32 v86, 0x43800000, v94
	v_mul_f32_e32 v50, 0x43800000, v54
	v_mul_f32_e32 v54, 0x43800000, v62
	s_waitcnt vmcnt(17)
	v_mul_f32_e32 v18, 0x43800000, v22
	s_waitcnt vmcnt(16)
	v_mul_f32_e32 v22, 0x43800000, v30
	v_med3_f32 v114, v114, s54, v192
	v_med3_f32 v118, v118, s54, v192
	v_med3_f32 v82, v82, s54, v192
	v_med3_f32 v86, v86, s54, v192
	v_med3_f32 v50, v50, s54, v192
	v_med3_f32 v54, v54, s54, v192
	v_med3_f32 v18, v18, s54, v192
	v_med3_f32 v22, v22, s54, v192
	v_cvt_pk_fp8_f32 v132, v114, v118 op_sel:[0,0,1]
	v_cvt_pk_fp8_f32 v133, v82, v86 op_sel:[0,0,1]
	v_cvt_pk_fp8_f32 v134, v50, v54 op_sel:[0,0,1]
	v_cvt_pk_fp8_f32 v135, v18, v22 op_sel:[0,0,1]
	s_add_i32 s1, s1, 0
	v_mul_u32_u24_e32 v2, 0x110, v131
	v_add3_u32 v1, s1, v1, v2
	v_mul_f32_e32 v2, 0x43800000, v83
	v_mul_f32_e32 v6, 0x43800000, v91
	ds_write_b128 v1, v[132:135]
	v_med3_f32 v2, v2, s54, v192
	v_med3_f32 v6, v6, s54, v192
	v_mov_b32_e32 v132, v163
	v_cvt_pk_fp8_f32 v132, v2, v6
	v_mul_f32_e32 v2, 0x43800000, v51
	v_mul_f32_e32 v6, 0x43800000, v59
	v_med3_f32 v2, v2, s54, v192
	v_med3_f32 v6, v6, s54, v192
	v_mov_b32_e32 v133, v163
	v_cvt_pk_fp8_f32 v133, v2, v6
	v_mul_f32_e32 v2, 0x43800000, v19
	v_mul_f32_e32 v6, 0x43800000, v27
	v_med3_f32 v2, v2, s54, v192
	v_med3_f32 v6, v6, s54, v192
	v_mov_b32_e32 v134, v163
	v_mul_f32_e32 v18, 0x43800000, v115
	v_mul_f32_e32 v22, 0x43800000, v119
	v_cvt_pk_fp8_f32 v134, v2, v6
	v_mul_f32_e32 v2, 0x43800000, v3
	v_mul_f32_e32 v3, 0x43800000, v7
	v_med3_f32 v18, v18, s54, v192
	v_med3_f32 v22, v22, s54, v192
	v_med3_f32 v2, v2, s54, v192
	v_med3_f32 v3, v3, s54, v192
	v_mov_b32_e32 v135, v163
	v_cvt_pk_fp8_f32 v132, v18, v22 op_sel:[0,0,1]
	v_mul_f32_e32 v18, 0x43800000, v87
	v_mul_f32_e32 v22, 0x43800000, v95
	v_cvt_pk_fp8_f32 v135, v2, v3
	v_med3_f32 v18, v18, s54, v192
	v_med3_f32 v22, v22, s54, v192
	v_cvt_pk_fp8_f32 v133, v18, v22 op_sel:[0,0,1]
	v_mul_f32_e32 v18, 0x43800000, v55
	v_mul_f32_e32 v19, 0x43800000, v63
	v_mul_f32_e32 v6, 0x43800000, v23
	v_mul_f32_e32 v7, 0x43800000, v31
	v_med3_f32 v18, v18, s54, v192
	v_med3_f32 v19, v19, s54, v192
	v_med3_f32 v6, v6, s54, v192
	v_med3_f32 v7, v7, s54, v192
	v_cvt_pk_fp8_f32 v134, v18, v19 op_sel:[0,0,1]
	v_cvt_pk_fp8_f32 v135, v6, v7 op_sel:[0,0,1]
	v_mul_f32_e32 v2, 0x43800000, v84
	v_mul_f32_e32 v3, 0x43800000, v92
	v_med3_f32 v2, v2, s54, v192
	ds_write_b128 v1, v[132:135] offset:272
	v_med3_f32 v3, v3, s54, v192
	v_mov_b32_e32 v132, v163
	v_cvt_pk_fp8_f32 v132, v2, v3
	v_mul_f32_e32 v2, 0x43800000, v52
	v_mul_f32_e32 v3, 0x43800000, v60
	v_med3_f32 v2, v2, s54, v192
	v_med3_f32 v3, v3, s54, v192
	v_mov_b32_e32 v133, v163
	v_mul_f32_e32 v6, 0x43800000, v116
	v_mul_f32_e32 v7, 0x43800000, v120
	v_cvt_pk_fp8_f32 v133, v2, v3
	v_mul_f32_e32 v2, 0x43800000, v20
	v_mul_f32_e32 v3, 0x43800000, v28
	v_med3_f32 v6, v6, s54, v192
	v_med3_f32 v7, v7, s54, v192
	v_med3_f32 v2, v2, s54, v192
	v_med3_f32 v3, v3, s54, v192
	v_mov_b32_e32 v134, v163
	v_cvt_pk_fp8_f32 v132, v6, v7 op_sel:[0,0,1]
	v_mul_f32_e32 v6, 0x43800000, v88
	v_mul_f32_e32 v7, 0x43800000, v96
	v_cvt_pk_fp8_f32 v134, v2, v3
	v_med3_f32 v6, v6, s54, v192
	v_med3_f32 v7, v7, s54, v192
	v_mul_f32_e32 v2, 0x43800000, v4
	v_mul_f32_e32 v3, 0x43800000, v8
	v_cvt_pk_fp8_f32 v133, v6, v7 op_sel:[0,0,1]
	v_mul_f32_e32 v6, 0x43800000, v56
	v_mul_f32_e32 v7, 0x43800000, v64
	v_med3_f32 v2, v2, s54, v192
	v_med3_f32 v3, v3, s54, v192
	v_mov_b32_e32 v135, v163
	v_med3_f32 v6, v6, s54, v192
	v_med3_f32 v7, v7, s54, v192
	v_cvt_pk_fp8_f32 v135, v2, v3
	v_mul_f32_e32 v2, 0x43800000, v85
	v_mul_f32_e32 v3, 0x43800000, v93
	v_cvt_pk_fp8_f32 v134, v6, v7 op_sel:[0,0,1]
	v_med3_f32 v7, v2, s54, v192
	v_med3_f32 v3, v3, s54, v192
	v_mov_b32_e32 v2, v163
	v_mul_f32_e32 v4, 0x43800000, v24
	v_mul_f32_e32 v6, 0x43800000, v32
	v_cvt_pk_fp8_f32 v2, v7, v3
	v_med3_f32 v4, v4, s54, v192
	v_med3_f32 v6, v6, s54, v192
	v_cvt_pk_fp8_f32 v135, v4, v6 op_sel:[0,0,1]
	v_mul_f32_e32 v4, 0x43800000, v117
	v_mul_f32_e32 v6, 0x43800000, v121
	v_med3_f32 v4, v4, s54, v192
	v_med3_f32 v6, v6, s54, v192
	v_cvt_pk_fp8_f32 v2, v4, v6 op_sel:[0,0,1]
	v_mul_f32_e32 v3, 0x43800000, v53
	v_mul_f32_e32 v4, 0x43800000, v61
	v_med3_f32 v8, v3, s54, v192
	v_med3_f32 v4, v4, s54, v192
	v_mov_b32_e32 v3, v163
	v_cvt_pk_fp8_f32 v3, v8, v4
	v_mul_f32_e32 v6, 0x43800000, v89
	v_mul_f32_e32 v7, 0x43800000, v97
	v_med3_f32 v6, v6, s54, v192
	v_med3_f32 v7, v7, s54, v192
	v_cvt_pk_fp8_f32 v3, v6, v7 op_sel:[0,0,1]
	v_mul_f32_e32 v4, 0x43800000, v21
	v_mul_f32_e32 v6, 0x43800000, v29
	v_med3_f32 v18, v4, s54, v192
	v_med3_f32 v6, v6, s54, v192
	v_mov_b32_e32 v4, v163
	v_cvt_pk_fp8_f32 v4, v18, v6
	v_mul_f32_e32 v5, 0x43800000, v5
	v_mul_f32_e32 v6, 0x43800000, v9
	v_med3_f32 v9, v5, s54, v192
	v_med3_f32 v6, v6, s54, v192
	v_mov_b32_e32 v5, v163
	v_mul_f32_e32 v7, 0x43800000, v57
	v_mul_f32_e32 v8, 0x43800000, v65
	v_cvt_pk_fp8_f32 v5, v9, v6
	v_med3_f32 v7, v7, s54, v192
	v_med3_f32 v8, v8, s54, v192
	v_cvt_pk_fp8_f32 v4, v7, v8 op_sel:[0,0,1]
	v_mul_f32_e32 v7, 0x43800000, v25
	v_mul_f32_e32 v8, 0x43800000, v33
	v_med3_f32 v7, v7, s54, v192
	v_med3_f32 v8, v8, s54, v192
	v_cvt_pk_fp8_f32 v5, v7, v8 op_sel:[0,0,1]
	ds_write_b128 v1, v[132:135] offset:544
	v_ashrrev_i32_e32 v132, 4, v130
	v_ashrrev_i32_e32 v133, 31, v132
	ds_write_b128 v1, v[2:5] offset:816
	v_lshlrev_b32_e32 v2, 4, v130
	v_and_b32_e32 v162, 0xf0, v2
	v_add_u32_e32 v2, 0x200, v130
	v_ashrrev_i32_e32 v136, 4, v2
	v_add_u32_e32 v2, 0x400, v130
	v_ashrrev_i32_e32 v140, 4, v2
	v_add_u32_e32 v2, 0x600, v130
	v_ashrrev_i32_e32 v144, 4, v2
	v_ashrrev_i32_e32 v137, 31, v136
	v_ashrrev_i32_e32 v141, 31, v140
	v_ashrrev_i32_e32 v145, 31, v144
	s_waitcnt lgkmcnt(0)
	s_barrier
	v_lshlrev_b64 v[134:135], 11, v[132:133]
	v_lshlrev_b64 v[138:139], 11, v[136:137]
	v_lshlrev_b64 v[142:143], 11, v[140:141]
	v_lshlrev_b64 v[160:161], 11, v[144:145]
	v_add_co_u32_e32 v2, vcc, s88, v164
	s_mov_b32 s1, 0x804000
	s_nop 0
	v_addc_co_u32_e32 v3, vcc, 0, v165, vcc
	v_add_co_u32_e32 v4, vcc, s1, v164
	s_mov_b32 s1, 0x808000
	s_nop 0
	v_addc_co_u32_e32 v5, vcc, 0, v165, vcc
	global_load_dwordx4 v[82:85], v[2:3], off sc0 nt
	global_load_dwordx4 v[90:93], v[4:5], off sc0 nt
	v_add_co_u32_e32 v2, vcc, s1, v164
	s_mov_b32 s1, 0x80c000
	s_nop 0
	v_addc_co_u32_e32 v3, vcc, 0, v165, vcc
	v_add_co_u32_e32 v4, vcc, s1, v164
	s_mov_b32 s1, 0x810000
	s_nop 0
	v_addc_co_u32_e32 v5, vcc, 0, v165, vcc
	global_load_dwordx4 v[114:117], v[2:3], off sc0 nt
	global_load_dwordx4 v[118:121], v[4:5], off sc0 nt
	v_add_co_u32_e32 v2, vcc, s1, v164
	s_mov_b32 s1, 0x814000
	s_nop 0
	v_addc_co_u32_e32 v3, vcc, 0, v165, vcc
	v_add_co_u32_e32 v4, vcc, s1, v164
	s_mov_b32 s1, 0x818000
	s_nop 0
	v_addc_co_u32_e32 v5, vcc, 0, v165, vcc
	global_load_dwordx4 v[50:53], v[2:3], off sc0 nt
	global_load_dwordx4 v[58:61], v[4:5], off sc0 nt
	v_add_co_u32_e32 v2, vcc, s1, v164
	s_mov_b32 s1, 0x81c000
	s_nop 0
	v_addc_co_u32_e32 v3, vcc, 0, v165, vcc
	v_add_co_u32_e32 v4, vcc, s1, v164
	s_mov_b32 s1, 0x820000
	s_nop 0
	v_addc_co_u32_e32 v5, vcc, 0, v165, vcc
	global_load_dwordx4 v[86:89], v[2:3], off sc0 nt
	global_load_dwordx4 v[94:97], v[4:5], off sc0 nt
	v_add_co_u32_e32 v2, vcc, s1, v164
	s_mov_b32 s1, 0x824000
	s_nop 0
	v_addc_co_u32_e32 v3, vcc, 0, v165, vcc
	v_add_co_u32_e32 v4, vcc, s1, v164
	s_mov_b32 s1, 0x828000
	s_nop 0
	v_addc_co_u32_e32 v5, vcc, 0, v165, vcc
	global_load_dwordx4 v[18:21], v[2:3], off sc0 nt
	global_load_dwordx4 v[26:29], v[4:5], off sc0 nt
	v_add_co_u32_e32 v2, vcc, s1, v164
	s_mov_b32 s1, 0x82c000
	s_nop 0
	v_addc_co_u32_e32 v3, vcc, 0, v165, vcc
	v_add_co_u32_e32 v4, vcc, s1, v164
	s_mov_b32 s1, 0x830000
	s_nop 0
	v_addc_co_u32_e32 v5, vcc, 0, v165, vcc
	global_load_dwordx4 v[54:57], v[2:3], off sc0 nt
	global_load_dwordx4 v[62:65], v[4:5], off sc0 nt
	v_add_co_u32_e32 v2, vcc, s1, v164
	s_mov_b32 s1, 0x834000
	s_nop 0
	v_addc_co_u32_e32 v3, vcc, 0, v165, vcc
	v_add_co_u32_e32 v6, vcc, s1, v164
	s_mov_b32 s1, 0x838000
	s_nop 0
	v_addc_co_u32_e32 v7, vcc, 0, v165, vcc
	v_add_co_u32_e32 v22, vcc, s1, v164
	s_mov_b32 s1, 0x83c000
	s_nop 0
	v_addc_co_u32_e32 v23, vcc, 0, v165, vcc
	v_add_co_u32_e32 v30, vcc, s1, v164
	global_load_dwordx4 v[2:5], v[2:3], off sc0 nt
	s_nop 0
	global_load_dwordx4 v[6:9], v[6:7], off sc0 nt
	v_addc_co_u32_e32 v31, vcc, 0, v165, vcc
	global_load_dwordx4 v[22:25], v[22:23], off sc0 nt
	s_nop 0
	global_load_dwordx4 v[30:33], v[30:31], off sc0 nt
	v_add_u32_e32 v158, 0, v162
	v_lshl_add_u64 v[166:167], s[8:9], 0, v[162:163]
	v_mad_u64_u32 v[146:147], s[8:9], v132, s55, v[158:159]
	ds_read_b128 v[130:133], v146
	v_lshl_add_u64 v[148:149], v[166:167], 0, v[134:135]
	v_mad_u64_u32 v[150:151], s[8:9], v136, s55, v[158:159]
	v_lshl_add_u64 v[152:153], v[166:167], 0, v[138:139]
	s_waitcnt lgkmcnt(0)
	global_store_dwordx4 v[148:149], v[130:133], off nt
	ds_read_b128 v[130:133], v150
	v_mad_u64_u32 v[154:155], s[8:9], v140, s55, v[158:159]
	v_lshl_add_u64 v[156:157], v[166:167], 0, v[142:143]
	v_mad_u64_u32 v[158:159], s[8:9], v144, s55, v[158:159]
	s_waitcnt lgkmcnt(0)
	global_store_dwordx4 v[152:153], v[130:133], off nt
	ds_read_b128 v[130:133], v154
	v_lshl_add_u64 v[160:161], v[166:167], 0, v[160:161]
	s_waitcnt lgkmcnt(0)
	global_store_dwordx4 v[156:157], v[130:133], off nt
	ds_read_b128 v[130:133], v158
	s_waitcnt lgkmcnt(0)
	global_store_dwordx4 v[160:161], v[130:133], off nt
	s_waitcnt vmcnt(35)
	v_mul_f32_e32 v98, 0x43800000, v98
	s_waitcnt vmcnt(34)
	v_mul_f32_e32 v106, 0x43800000, v106
	s_waitcnt vmcnt(31)
	v_mul_f32_e32 v66, 0x43800000, v66
	s_waitcnt vmcnt(30)
	v_mul_f32_e32 v74, 0x43800000, v74
	s_waitcnt vmcnt(27)
	v_mul_f32_e32 v34, 0x43800000, v34
	s_waitcnt vmcnt(26)
	v_mul_f32_e32 v42, 0x43800000, v42
	s_waitcnt vmcnt(23)
	v_mul_f32_e32 v10, 0x43800000, v10
	s_waitcnt vmcnt(22)
	v_mul_f32_e32 v14, 0x43800000, v14
	v_med3_f32 v98, v98, s54, v192
	v_med3_f32 v106, v106, s54, v192
	v_mov_b32_e32 v130, v163
	v_med3_f32 v66, v66, s54, v192
	v_med3_f32 v74, v74, s54, v192
	v_mov_b32_e32 v131, v163
	v_med3_f32 v34, v34, s54, v192
	v_med3_f32 v42, v42, s54, v192
	v_mov_b32_e32 v132, v163
	v_med3_f32 v10, v10, s54, v192
	v_med3_f32 v14, v14, s54, v192
	v_mov_b32_e32 v133, v163
	v_cvt_pk_fp8_f32 v130, v98, v106
	v_cvt_pk_fp8_f32 v131, v66, v74
	v_cvt_pk_fp8_f32 v132, v34, v42
	v_cvt_pk_fp8_f32 v133, v10, v14
	v_mul_f32_e32 v122, 0x43800000, v122
	v_mul_f32_e32 v126, 0x43800000, v126
	v_mul_f32_e32 v98, 0x43800000, v102
	v_mul_f32_e32 v102, 0x43800000, v110
	v_mul_f32_e32 v66, 0x43800000, v70
	v_mul_f32_e32 v70, 0x43800000, v78
	s_waitcnt vmcnt(21)
	v_mul_f32_e32 v34, 0x43800000, v38
	s_waitcnt vmcnt(20)
	v_mul_f32_e32 v38, 0x43800000, v46
	v_med3_f32 v122, v122, s54, v192
	v_med3_f32 v126, v126, s54, v192
	v_med3_f32 v98, v98, s54, v192
	v_med3_f32 v102, v102, s54, v192
	v_med3_f32 v66, v66, s54, v192
	v_med3_f32 v70, v70, s54, v192
	v_med3_f32 v34, v34, s54, v192
	v_med3_f32 v38, v38, s54, v192
	v_cvt_pk_fp8_f32 v130, v122, v126 op_sel:[0,0,1]
	v_cvt_pk_fp8_f32 v131, v98, v102 op_sel:[0,0,1]
	v_cvt_pk_fp8_f32 v132, v66, v70 op_sel:[0,0,1]
	v_cvt_pk_fp8_f32 v133, v34, v38 op_sel:[0,0,1]
	v_mul_f32_e32 v10, 0x43800000, v99
	v_mul_f32_e32 v14, 0x43800000, v107
	v_med3_f32 v10, v10, s54, v192
	ds_write_b128 v1, v[130:133] offset:34816
	v_med3_f32 v14, v14, s54, v192
	v_mov_b32_e32 v130, v163
	v_cvt_pk_fp8_f32 v130, v10, v14
	v_mul_f32_e32 v10, 0x43800000, v67
	v_mul_f32_e32 v14, 0x43800000, v75
	v_med3_f32 v10, v10, s54, v192
	v_med3_f32 v14, v14, s54, v192
	v_mov_b32_e32 v131, v163
	v_cvt_pk_fp8_f32 v131, v10, v14
	v_mul_f32_e32 v10, 0x43800000, v35
	v_mul_f32_e32 v14, 0x43800000, v43
	v_med3_f32 v10, v10, s54, v192
	v_med3_f32 v14, v14, s54, v192
	v_mov_b32_e32 v132, v163
	v_mul_f32_e32 v34, 0x43800000, v123
	v_mul_f32_e32 v38, 0x43800000, v127
	v_cvt_pk_fp8_f32 v132, v10, v14
	v_mul_f32_e32 v10, 0x43800000, v11
	v_mul_f32_e32 v11, 0x43800000, v15
	v_med3_f32 v34, v34, s54, v192
	v_med3_f32 v38, v38, s54, v192
	v_med3_f32 v10, v10, s54, v192
	v_med3_f32 v11, v11, s54, v192
	v_mov_b32_e32 v133, v163
	v_cvt_pk_fp8_f32 v130, v34, v38 op_sel:[0,0,1]
	v_mul_f32_e32 v34, 0x43800000, v103
	v_mul_f32_e32 v38, 0x43800000, v111
	v_cvt_pk_fp8_f32 v133, v10, v11
	v_med3_f32 v34, v34, s54, v192
	v_med3_f32 v38, v38, s54, v192
	v_cvt_pk_fp8_f32 v131, v34, v38 op_sel:[0,0,1]
	v_mul_f32_e32 v34, 0x43800000, v71
	v_mul_f32_e32 v35, 0x43800000, v79
	v_mul_f32_e32 v14, 0x43800000, v39
	v_mul_f32_e32 v15, 0x43800000, v47
	v_med3_f32 v34, v34, s54, v192
	v_med3_f32 v35, v35, s54, v192
	v_med3_f32 v14, v14, s54, v192
	v_med3_f32 v15, v15, s54, v192
	v_cvt_pk_fp8_f32 v132, v34, v35 op_sel:[0,0,1]
	v_cvt_pk_fp8_f32 v133, v14, v15 op_sel:[0,0,1]
	v_mul_f32_e32 v10, 0x43800000, v100
	v_mul_f32_e32 v11, 0x43800000, v108
	v_med3_f32 v10, v10, s54, v192
	ds_write_b128 v1, v[130:133] offset:35088
	v_med3_f32 v11, v11, s54, v192
	v_mov_b32_e32 v130, v163
	v_cvt_pk_fp8_f32 v130, v10, v11
	v_mul_f32_e32 v10, 0x43800000, v68
	v_mul_f32_e32 v11, 0x43800000, v76
	v_med3_f32 v10, v10, s54, v192
	v_med3_f32 v11, v11, s54, v192
	v_mov_b32_e32 v131, v163
	v_mul_f32_e32 v14, 0x43800000, v124
	v_mul_f32_e32 v15, 0x43800000, v128
	v_cvt_pk_fp8_f32 v131, v10, v11
	v_mul_f32_e32 v10, 0x43800000, v36
	v_mul_f32_e32 v11, 0x43800000, v44
	v_med3_f32 v14, v14, s54, v192
	v_med3_f32 v15, v15, s54, v192
	v_med3_f32 v10, v10, s54, v192
	v_med3_f32 v11, v11, s54, v192
	v_mov_b32_e32 v132, v163
	v_cvt_pk_fp8_f32 v130, v14, v15 op_sel:[0,0,1]
	v_mul_f32_e32 v14, 0x43800000, v104
	v_mul_f32_e32 v15, 0x43800000, v112
	v_cvt_pk_fp8_f32 v132, v10, v11
	v_med3_f32 v14, v14, s54, v192
	v_med3_f32 v15, v15, s54, v192
	v_mul_f32_e32 v10, 0x43800000, v12
	v_mul_f32_e32 v11, 0x43800000, v16
	v_cvt_pk_fp8_f32 v131, v14, v15 op_sel:[0,0,1]
	v_mul_f32_e32 v14, 0x43800000, v72
	v_mul_f32_e32 v15, 0x43800000, v80
	v_med3_f32 v10, v10, s54, v192
	v_med3_f32 v11, v11, s54, v192
	v_mov_b32_e32 v133, v163
	v_med3_f32 v14, v14, s54, v192
	v_med3_f32 v15, v15, s54, v192
	v_cvt_pk_fp8_f32 v133, v10, v11
	v_mul_f32_e32 v10, 0x43800000, v101
	v_mul_f32_e32 v11, 0x43800000, v109
	v_cvt_pk_fp8_f32 v132, v14, v15 op_sel:[0,0,1]
	v_med3_f32 v15, v10, s54, v192
	v_med3_f32 v11, v11, s54, v192
	v_mov_b32_e32 v10, v163
	v_mul_f32_e32 v12, 0x43800000, v40
	v_mul_f32_e32 v14, 0x43800000, v48
	v_cvt_pk_fp8_f32 v10, v15, v11
	v_med3_f32 v12, v12, s54, v192
	v_med3_f32 v14, v14, s54, v192
	v_cvt_pk_fp8_f32 v133, v12, v14 op_sel:[0,0,1]
	v_mul_f32_e32 v12, 0x43800000, v125
	v_mul_f32_e32 v14, 0x43800000, v129
	v_med3_f32 v12, v12, s54, v192
	v_med3_f32 v14, v14, s54, v192
	v_cvt_pk_fp8_f32 v10, v12, v14 op_sel:[0,0,1]
	v_mul_f32_e32 v11, 0x43800000, v69
	v_mul_f32_e32 v12, 0x43800000, v77
	v_med3_f32 v16, v11, s54, v192
	v_med3_f32 v12, v12, s54, v192
	v_mov_b32_e32 v11, v163
	v_cvt_pk_fp8_f32 v11, v16, v12
	v_mul_f32_e32 v14, 0x43800000, v105
	v_mul_f32_e32 v15, 0x43800000, v113
	v_med3_f32 v14, v14, s54, v192
	v_med3_f32 v15, v15, s54, v192
	v_cvt_pk_fp8_f32 v11, v14, v15 op_sel:[0,0,1]
	v_mul_f32_e32 v12, 0x43800000, v37
	v_mul_f32_e32 v14, 0x43800000, v45
	v_med3_f32 v34, v12, s54, v192
	v_med3_f32 v14, v14, s54, v192
	v_mov_b32_e32 v12, v163
	v_cvt_pk_fp8_f32 v12, v34, v14
	v_mul_f32_e32 v13, 0x43800000, v13
	v_mul_f32_e32 v14, 0x43800000, v17
	v_med3_f32 v17, v13, s54, v192
	v_med3_f32 v14, v14, s54, v192
	v_mov_b32_e32 v13, v163
	v_mul_f32_e32 v15, 0x43800000, v73
	v_mul_f32_e32 v16, 0x43800000, v81
	v_cvt_pk_fp8_f32 v13, v17, v14
	v_med3_f32 v15, v15, s54, v192
	v_med3_f32 v16, v16, s54, v192
	v_cvt_pk_fp8_f32 v12, v15, v16 op_sel:[0,0,1]
	v_mul_f32_e32 v15, 0x43800000, v41
	v_mul_f32_e32 v16, 0x43800000, v49
	v_med3_f32 v15, v15, s54, v192
	v_med3_f32 v16, v16, s54, v192
	v_cvt_pk_fp8_f32 v13, v15, v16 op_sel:[0,0,1]
	ds_write_b128 v1, v[130:133] offset:35360
	ds_write_b128 v1, v[10:13] offset:35632
	s_waitcnt lgkmcnt(0)
	s_barrier
	s_mov_b32 s1, 0xc00000
	v_add_co_u32_e32 v10, vcc, s1, v164
	s_mov_b32 s1, 0xc04000
	s_nop 0
	v_addc_co_u32_e32 v11, vcc, 0, v165, vcc
	v_add_co_u32_e32 v12, vcc, s1, v164
	s_mov_b32 s1, 0xc08000
	s_nop 0
	v_addc_co_u32_e32 v13, vcc, 0, v165, vcc
	global_load_dwordx4 v[102:105], v[10:11], off sc0 nt
	global_load_dwordx4 v[122:125], v[12:13], off sc0 nt
	v_add_co_u32_e32 v10, vcc, s1, v164
	s_mov_b32 s1, 0xc0c000
	s_nop 0
	v_addc_co_u32_e32 v11, vcc, 0, v165, vcc
	v_add_co_u32_e32 v12, vcc, s1, v164
	s_mov_b32 s1, 0xc10000
	s_nop 0
	v_addc_co_u32_e32 v13, vcc, 0, v165, vcc
	global_load_dwordx4 v[130:133], v[10:11], off sc0 nt
	global_load_dwordx4 v[138:141], v[12:13], off sc0 nt
	v_add_co_u32_e32 v10, vcc, s1, v164
	s_mov_b32 s1, 0xc14000
	s_nop 0
	v_addc_co_u32_e32 v11, vcc, 0, v165, vcc
	v_add_co_u32_e32 v12, vcc, s1, v164
	s_mov_b32 s1, 0xc18000
	s_nop 0
	v_addc_co_u32_e32 v13, vcc, 0, v165, vcc
	global_load_dwordx4 v[70:73], v[10:11], off sc0 nt
	global_load_dwordx4 v[78:81], v[12:13], off sc0 nt
	v_add_co_u32_e32 v10, vcc, s1, v164
	s_mov_b32 s1, 0xc1c000
	s_nop 0
	v_addc_co_u32_e32 v11, vcc, 0, v165, vcc
	v_add_co_u32_e32 v12, vcc, s1, v164
	s_mov_b32 s1, 0xc20000
	s_nop 0
	v_addc_co_u32_e32 v13, vcc, 0, v165, vcc
	global_load_dwordx4 v[106:109], v[10:11], off sc0 nt
	global_load_dwordx4 v[126:129], v[12:13], off sc0 nt
	v_add_co_u32_e32 v10, vcc, s1, v164
	s_mov_b32 s1, 0xc24000
	s_nop 0
	v_addc_co_u32_e32 v11, vcc, 0, v165, vcc
	v_add_co_u32_e32 v12, vcc, s1, v164
	s_mov_b32 s1, 0xc28000
	s_nop 0
	v_addc_co_u32_e32 v13, vcc, 0, v165, vcc
	global_load_dwordx4 v[34:37], v[10:11], off sc0 nt
	global_load_dwordx4 v[42:45], v[12:13], off sc0 nt
	v_add_co_u32_e32 v10, vcc, s1, v164
	s_mov_b32 s1, 0xc2c000
	s_nop 0
	v_addc_co_u32_e32 v11, vcc, 0, v165, vcc
	v_add_co_u32_e32 v12, vcc, s1, v164
	s_mov_b32 s1, 0xc30000
	s_nop 0
	v_addc_co_u32_e32 v13, vcc, 0, v165, vcc
	global_load_dwordx4 v[74:77], v[10:11], off sc0 nt
	global_load_dwordx4 v[98:101], v[12:13], off sc0 nt
	v_add_co_u32_e32 v10, vcc, s1, v164
	s_mov_b32 s1, 0xc34000
	s_nop 0
	v_addc_co_u32_e32 v11, vcc, 0, v165, vcc
	v_add_co_u32_e32 v14, vcc, s1, v164
	s_mov_b32 s1, 0xc38000
	s_nop 0
	v_addc_co_u32_e32 v15, vcc, 0, v165, vcc
	v_add_co_u32_e32 v38, vcc, s1, v164
	s_mov_b32 s1, 0xc3c000
	s_nop 0
	v_addc_co_u32_e32 v39, vcc, 0, v165, vcc
	v_add_co_u32_e32 v46, vcc, s1, v164
	global_load_dwordx4 v[10:13], v[10:11], off sc0 nt
	s_nop 0
	global_load_dwordx4 v[14:17], v[14:15], off sc0 nt
	v_addc_co_u32_e32 v47, vcc, 0, v165, vcc
	global_load_dwordx4 v[38:41], v[38:39], off sc0 nt
	s_nop 0
	global_load_dwordx4 v[66:69], v[46:47], off sc0 nt
	ds_read_b128 v[46:49], v146 offset:34816
	s_waitcnt lgkmcnt(0)
	global_store_dwordx4 v[148:149], v[46:49], off offset:256 nt
	ds_read_b128 v[46:49], v150 offset:34816
	s_waitcnt lgkmcnt(0)
	global_store_dwordx4 v[152:153], v[46:49], off offset:256 nt
	ds_read_b128 v[46:49], v154 offset:34816
	s_waitcnt lgkmcnt(0)
	global_store_dwordx4 v[156:157], v[46:49], off offset:256 nt
	ds_read_b128 v[46:49], v158 offset:34816
	s_waitcnt lgkmcnt(0)
	global_store_dwordx4 v[160:161], v[46:49], off offset:256 nt
	s_waitcnt vmcnt(39)
	s_nop 0
	v_mul_f32_e32 v46, 0x43800000, v82
	s_waitcnt vmcnt(38)
	v_mul_f32_e32 v47, 0x43800000, v90
	v_med3_f32 v82, v46, s54, v192
	v_med3_f32 v47, v47, s54, v192
	v_mov_b32_e32 v46, v163
	v_cvt_pk_fp8_f32 v46, v82, v47
	s_waitcnt vmcnt(37)
	v_mul_f32_e32 v48, 0x43800000, v114
	s_waitcnt vmcnt(36)
	v_mul_f32_e32 v49, 0x43800000, v118
	v_med3_f32 v48, v48, s54, v192
	v_med3_f32 v49, v49, s54, v192
	v_cvt_pk_fp8_f32 v46, v48, v49 op_sel:[0,0,1]
	s_waitcnt vmcnt(35)
	v_mul_f32_e32 v47, 0x43800000, v50
	s_waitcnt vmcnt(34)
	v_mul_f32_e32 v48, 0x43800000, v58
	v_med3_f32 v58, v47, s54, v192
	v_med3_f32 v48, v48, s54, v192
	v_mov_b32_e32 v47, v163
	v_cvt_pk_fp8_f32 v47, v58, v48
	s_waitcnt vmcnt(33)
	v_mul_f32_e32 v49, 0x43800000, v86
	s_waitcnt vmcnt(32)
	v_mul_f32_e32 v50, 0x43800000, v94
	v_med3_f32 v49, v49, s54, v192
	v_med3_f32 v50, v50, s54, v192
	s_waitcnt vmcnt(31)
	v_mul_f32_e32 v18, 0x43800000, v18
	s_waitcnt vmcnt(30)
	v_mul_f32_e32 v26, 0x43800000, v26
	s_waitcnt vmcnt(29)
	v_mul_f32_e32 v48, 0x43800000, v54
	v_cvt_pk_fp8_f32 v47, v49, v50 op_sel:[0,0,1]
	v_med3_f32 v18, v18, s54, v192
	v_med3_f32 v26, v26, s54, v192
	v_med3_f32 v50, v48, s54, v192
	v_mov_b32_e32 v48, v163
	v_cvt_pk_fp8_f32 v48, v18, v26
	s_waitcnt vmcnt(28)
	v_mul_f32_e32 v49, 0x43800000, v62
	v_med3_f32 v49, v49, s54, v192
	s_waitcnt vmcnt(27)
	v_mul_f32_e32 v2, 0x43800000, v2
	s_waitcnt vmcnt(26)
	v_mul_f32_e32 v6, 0x43800000, v6
	v_cvt_pk_fp8_f32 v48, v50, v49 op_sel:[0,0,1]
	v_med3_f32 v2, v2, s54, v192
	v_med3_f32 v6, v6, s54, v192
	v_mov_b32_e32 v49, v163
	v_cvt_pk_fp8_f32 v49, v2, v6
	s_waitcnt vmcnt(25)
	v_mul_f32_e32 v18, 0x43800000, v22
	s_waitcnt vmcnt(24)
	v_mul_f32_e32 v22, 0x43800000, v30
	v_med3_f32 v18, v18, s54, v192
	v_med3_f32 v22, v22, s54, v192
	v_cvt_pk_fp8_f32 v49, v18, v22 op_sel:[0,0,1]
	v_mul_f32_e32 v2, 0x43800000, v83
	v_mul_f32_e32 v6, 0x43800000, v91
	v_med3_f32 v2, v2, s54, v192
	ds_write_b128 v1, v[46:49]
	v_med3_f32 v6, v6, s54, v192
	v_mov_b32_e32 v46, v163
	v_cvt_pk_fp8_f32 v46, v2, v6
	v_mul_f32_e32 v2, 0x43800000, v51
	v_mul_f32_e32 v6, 0x43800000, v59
	v_med3_f32 v2, v2, s54, v192
	v_med3_f32 v6, v6, s54, v192
	v_mov_b32_e32 v47, v163
	v_cvt_pk_fp8_f32 v47, v2, v6
	v_mul_f32_e32 v2, 0x43800000, v19
	v_mul_f32_e32 v6, 0x43800000, v27
	v_med3_f32 v2, v2, s54, v192
	v_med3_f32 v6, v6, s54, v192
	v_mov_b32_e32 v48, v163
	v_mul_f32_e32 v18, 0x43800000, v115
	v_mul_f32_e32 v22, 0x43800000, v119
	v_cvt_pk_fp8_f32 v48, v2, v6
	v_mul_f32_e32 v2, 0x43800000, v3
	v_mul_f32_e32 v3, 0x43800000, v7
	v_med3_f32 v18, v18, s54, v192
	v_med3_f32 v22, v22, s54, v192
	v_med3_f32 v2, v2, s54, v192
	v_med3_f32 v3, v3, s54, v192
	v_mov_b32_e32 v49, v163
	v_cvt_pk_fp8_f32 v46, v18, v22 op_sel:[0,0,1]
	v_mul_f32_e32 v18, 0x43800000, v87
	v_mul_f32_e32 v22, 0x43800000, v95
	v_cvt_pk_fp8_f32 v49, v2, v3
	v_med3_f32 v18, v18, s54, v192
	v_med3_f32 v22, v22, s54, v192
	v_cvt_pk_fp8_f32 v47, v18, v22 op_sel:[0,0,1]
	v_mul_f32_e32 v18, 0x43800000, v55
	v_mul_f32_e32 v19, 0x43800000, v63
	v_mul_f32_e32 v6, 0x43800000, v23
	v_mul_f32_e32 v7, 0x43800000, v31
	v_med3_f32 v18, v18, s54, v192
	v_med3_f32 v19, v19, s54, v192
	v_med3_f32 v6, v6, s54, v192
	v_med3_f32 v7, v7, s54, v192
	v_cvt_pk_fp8_f32 v48, v18, v19 op_sel:[0,0,1]
	v_cvt_pk_fp8_f32 v49, v6, v7 op_sel:[0,0,1]
	v_mul_f32_e32 v2, 0x43800000, v84
	v_mul_f32_e32 v3, 0x43800000, v92
	v_med3_f32 v2, v2, s54, v192
	ds_write_b128 v1, v[46:49] offset:272
	v_med3_f32 v3, v3, s54, v192
	v_mov_b32_e32 v46, v163
	v_cvt_pk_fp8_f32 v46, v2, v3
	v_mul_f32_e32 v2, 0x43800000, v52
	v_mul_f32_e32 v3, 0x43800000, v60
	v_med3_f32 v2, v2, s54, v192
	v_med3_f32 v3, v3, s54, v192
	v_mov_b32_e32 v47, v163
	v_mul_f32_e32 v6, 0x43800000, v116
	v_mul_f32_e32 v7, 0x43800000, v120
	v_cvt_pk_fp8_f32 v47, v2, v3
	v_mul_f32_e32 v2, 0x43800000, v20
	v_mul_f32_e32 v3, 0x43800000, v28
	v_med3_f32 v6, v6, s54, v192
	v_med3_f32 v7, v7, s54, v192
	v_med3_f32 v2, v2, s54, v192
	v_med3_f32 v3, v3, s54, v192
	v_mov_b32_e32 v48, v163
	v_cvt_pk_fp8_f32 v46, v6, v7 op_sel:[0,0,1]
	v_mul_f32_e32 v6, 0x43800000, v88
	v_mul_f32_e32 v7, 0x43800000, v96
	v_cvt_pk_fp8_f32 v48, v2, v3
	v_med3_f32 v6, v6, s54, v192
	v_med3_f32 v7, v7, s54, v192
	v_mul_f32_e32 v2, 0x43800000, v4
	v_mul_f32_e32 v3, 0x43800000, v8
	v_cvt_pk_fp8_f32 v47, v6, v7 op_sel:[0,0,1]
	v_mul_f32_e32 v6, 0x43800000, v56
	v_mul_f32_e32 v7, 0x43800000, v64
	v_med3_f32 v2, v2, s54, v192
	v_med3_f32 v3, v3, s54, v192
	v_mov_b32_e32 v49, v163
	v_med3_f32 v6, v6, s54, v192
	v_med3_f32 v7, v7, s54, v192
	v_cvt_pk_fp8_f32 v49, v2, v3
	v_mul_f32_e32 v2, 0x43800000, v85
	v_mul_f32_e32 v3, 0x43800000, v93
	v_cvt_pk_fp8_f32 v48, v6, v7 op_sel:[0,0,1]
	v_med3_f32 v7, v2, s54, v192
	v_med3_f32 v3, v3, s54, v192
	v_mov_b32_e32 v2, v163
	v_mul_f32_e32 v4, 0x43800000, v24
	v_mul_f32_e32 v6, 0x43800000, v32
	v_cvt_pk_fp8_f32 v2, v7, v3
	v_med3_f32 v4, v4, s54, v192
	v_med3_f32 v6, v6, s54, v192
	v_cvt_pk_fp8_f32 v49, v4, v6 op_sel:[0,0,1]
	v_mul_f32_e32 v4, 0x43800000, v117
	v_mul_f32_e32 v6, 0x43800000, v121
	v_med3_f32 v4, v4, s54, v192
	v_med3_f32 v6, v6, s54, v192
	v_cvt_pk_fp8_f32 v2, v4, v6 op_sel:[0,0,1]
	v_mul_f32_e32 v3, 0x43800000, v53
	v_mul_f32_e32 v4, 0x43800000, v61
	v_med3_f32 v8, v3, s54, v192
	v_med3_f32 v4, v4, s54, v192
	v_mov_b32_e32 v3, v163
	v_cvt_pk_fp8_f32 v3, v8, v4
	v_mul_f32_e32 v6, 0x43800000, v89
	v_mul_f32_e32 v7, 0x43800000, v97
	v_med3_f32 v6, v6, s54, v192
	v_med3_f32 v7, v7, s54, v192
	v_cvt_pk_fp8_f32 v3, v6, v7 op_sel:[0,0,1]
	v_mul_f32_e32 v4, 0x43800000, v21
	v_mul_f32_e32 v6, 0x43800000, v29
	v_med3_f32 v18, v4, s54, v192
	v_med3_f32 v6, v6, s54, v192
	v_mov_b32_e32 v4, v163
	v_cvt_pk_fp8_f32 v4, v18, v6
	v_mul_f32_e32 v5, 0x43800000, v5
	v_mul_f32_e32 v6, 0x43800000, v9
	v_med3_f32 v9, v5, s54, v192
	v_med3_f32 v6, v6, s54, v192
	v_mov_b32_e32 v5, v163
	v_mul_f32_e32 v7, 0x43800000, v57
	v_mul_f32_e32 v8, 0x43800000, v65
	v_cvt_pk_fp8_f32 v5, v9, v6
	v_med3_f32 v7, v7, s54, v192
	v_med3_f32 v8, v8, s54, v192
	v_cvt_pk_fp8_f32 v4, v7, v8 op_sel:[0,0,1]
	v_mul_f32_e32 v7, 0x43800000, v25
	v_mul_f32_e32 v8, 0x43800000, v33
	v_med3_f32 v7, v7, s54, v192
	v_med3_f32 v8, v8, s54, v192
	v_cvt_pk_fp8_f32 v5, v7, v8 op_sel:[0,0,1]
	ds_write_b128 v1, v[46:49] offset:544
	ds_write_b128 v1, v[2:5] offset:816
	s_waitcnt lgkmcnt(0)
	s_barrier
	s_mov_b32 s1, 0x1000000
	v_add_co_u32_e32 v2, vcc, s1, v164
	s_mov_b32 s1, 0x1004000
	s_nop 0
	v_addc_co_u32_e32 v3, vcc, 0, v165, vcc
	v_add_co_u32_e32 v4, vcc, s1, v164
	s_mov_b32 s1, 0x1008000
	s_nop 0
	v_addc_co_u32_e32 v5, vcc, 0, v165, vcc
	global_load_dwordx4 v[90:93], v[2:3], off sc0 nt
	global_load_dwordx4 v[114:117], v[4:5], off sc0 nt
	v_add_co_u32_e32 v2, vcc, s1, v164
	s_mov_b32 s1, 0x100c000
	s_nop 0
	v_addc_co_u32_e32 v3, vcc, 0, v165, vcc
	v_add_co_u32_e32 v4, vcc, s1, v164
	s_mov_b32 s1, 0x1010000
	s_nop 0
	v_addc_co_u32_e32 v5, vcc, 0, v165, vcc
	global_load_dwordx4 v[134:137], v[2:3], off sc0 nt
	global_load_dwordx4 v[142:145], v[4:5], off sc0 nt
	v_add_co_u32_e32 v2, vcc, s1, v164
	s_mov_b32 s1, 0x1014000
	s_nop 0
	v_addc_co_u32_e32 v3, vcc, 0, v165, vcc
	v_add_co_u32_e32 v4, vcc, s1, v164
	s_mov_b32 s1, 0x1018000
	s_nop 0
	v_addc_co_u32_e32 v5, vcc, 0, v165, vcc
	global_load_dwordx4 v[54:57], v[2:3], off sc0 nt
	global_load_dwordx4 v[82:85], v[4:5], off sc0 nt
	v_add_co_u32_e32 v2, vcc, s1, v164
	s_mov_b32 s1, 0x101c000
	s_nop 0
	v_addc_co_u32_e32 v3, vcc, 0, v165, vcc
	v_add_co_u32_e32 v4, vcc, s1, v164
	s_mov_b32 s1, 0x1020000
	s_nop 0
	v_addc_co_u32_e32 v5, vcc, 0, v165, vcc
	global_load_dwordx4 v[110:113], v[2:3], off sc0 nt
	global_load_dwordx4 v[118:121], v[4:5], off sc0 nt
	v_add_co_u32_e32 v2, vcc, s1, v164
	s_mov_b32 s1, 0x1024000
	s_nop 0
	v_addc_co_u32_e32 v3, vcc, 0, v165, vcc
	v_add_co_u32_e32 v4, vcc, s1, v164
	s_mov_b32 s1, 0x1028000
	s_nop 0
	v_addc_co_u32_e32 v5, vcc, 0, v165, vcc
	global_load_dwordx4 v[22:25], v[2:3], off sc0 nt
	global_load_dwordx4 v[46:49], v[4:5], off sc0 nt
	v_add_co_u32_e32 v2, vcc, s1, v164
	s_mov_b32 s1, 0x102c000
	s_nop 0
	v_addc_co_u32_e32 v3, vcc, 0, v165, vcc
	v_add_co_u32_e32 v4, vcc, s1, v164
	s_mov_b32 s1, 0x1030000
	s_nop 0
	v_addc_co_u32_e32 v5, vcc, 0, v165, vcc
	global_load_dwordx4 v[62:65], v[2:3], off sc0 nt
	global_load_dwordx4 v[86:89], v[4:5], off sc0 nt
	v_add_co_u32_e32 v2, vcc, s1, v164
	s_mov_b32 s1, 0x1034000
	s_nop 0
	v_addc_co_u32_e32 v3, vcc, 0, v165, vcc
	v_add_co_u32_e32 v6, vcc, s1, v164
	s_mov_b32 s1, 0x1038000
	s_nop 0
	v_addc_co_u32_e32 v7, vcc, 0, v165, vcc
	global_load_dwordx4 v[2:5], v[2:3], off sc0 nt
	s_nop 0
	global_load_dwordx4 v[18:21], v[6:7], off sc0 nt
	v_add_co_u32_e32 v6, vcc, s1, v164
	s_mov_b32 s1, 0x103c000
	s_nop 0
	v_addc_co_u32_e32 v7, vcc, 0, v165, vcc
	v_add_co_u32_e32 v8, vcc, s1, v164
	s_nop 1
	v_addc_co_u32_e32 v9, vcc, 0, v165, vcc
	global_load_dwordx4 v[30:33], v[6:7], off sc0 nt
	global_load_dwordx4 v[50:53], v[8:9], off sc0 nt
	ds_read_b128 v[6:9], v146
	s_waitcnt lgkmcnt(0)
	global_store_dwordx4 v[148:149], v[6:9], off offset:512 nt
	ds_read_b128 v[6:9], v150
	s_waitcnt lgkmcnt(0)
	global_store_dwordx4 v[152:153], v[6:9], off offset:512 nt
	ds_read_b128 v[6:9], v154
	s_waitcnt lgkmcnt(0)
	global_store_dwordx4 v[156:157], v[6:9], off offset:512 nt
	ds_read_b128 v[6:9], v158
	s_waitcnt lgkmcnt(0)
	global_store_dwordx4 v[160:161], v[6:9], off offset:512 nt
	s_waitcnt vmcnt(39)
	s_nop 0
	v_mul_f32_e32 v6, 0x43800000, v102
	s_waitcnt vmcnt(38)
	v_mul_f32_e32 v7, 0x43800000, v122
	v_med3_f32 v26, v6, s54, v192
	v_med3_f32 v7, v7, s54, v192
	v_mov_b32_e32 v6, v163
	v_cvt_pk_fp8_f32 v6, v26, v7
	s_waitcnt vmcnt(37)
	v_mul_f32_e32 v8, 0x43800000, v130
	s_waitcnt vmcnt(36)
	v_mul_f32_e32 v9, 0x43800000, v138
	v_med3_f32 v8, v8, s54, v192
	v_med3_f32 v9, v9, s54, v192
	v_cvt_pk_fp8_f32 v6, v8, v9 op_sel:[0,0,1]
	s_waitcnt vmcnt(35)
	v_mul_f32_e32 v7, 0x43800000, v70
	s_waitcnt vmcnt(34)
	v_mul_f32_e32 v8, 0x43800000, v78
	v_med3_f32 v27, v7, s54, v192
	v_med3_f32 v8, v8, s54, v192
	v_mov_b32_e32 v7, v163
	v_cvt_pk_fp8_f32 v7, v27, v8
	s_waitcnt vmcnt(33)
	v_mul_f32_e32 v9, 0x43800000, v106
	s_waitcnt vmcnt(32)
	v_mul_f32_e32 v26, 0x43800000, v126
	v_med3_f32 v9, v9, s54, v192
	v_med3_f32 v26, v26, s54, v192
	v_cvt_pk_fp8_f32 v7, v9, v26 op_sel:[0,0,1]
	s_waitcnt vmcnt(31)
	v_mul_f32_e32 v8, 0x43800000, v34
	s_waitcnt vmcnt(30)
	v_mul_f32_e32 v9, 0x43800000, v42
	v_med3_f32 v28, v8, s54, v192
	v_med3_f32 v9, v9, s54, v192
	v_mov_b32_e32 v8, v163
	v_cvt_pk_fp8_f32 v8, v28, v9
	s_waitcnt vmcnt(29)
	v_mul_f32_e32 v26, 0x43800000, v74
	s_waitcnt vmcnt(28)
	v_mul_f32_e32 v27, 0x43800000, v98
	v_med3_f32 v26, v26, s54, v192
	v_med3_f32 v27, v27, s54, v192
	s_waitcnt vmcnt(27)
	v_mul_f32_e32 v9, 0x43800000, v10
	s_waitcnt vmcnt(26)
	v_mul_f32_e32 v10, 0x43800000, v14
	v_cvt_pk_fp8_f32 v8, v26, v27 op_sel:[0,0,1]
	v_med3_f32 v27, v9, s54, v192
	v_med3_f32 v10, v10, s54, v192
	v_mov_b32_e32 v9, v163
	v_cvt_pk_fp8_f32 v9, v27, v10
	s_waitcnt vmcnt(25)
	v_mul_f32_e32 v14, 0x43800000, v38
	s_waitcnt vmcnt(24)
	v_mul_f32_e32 v26, 0x43800000, v66
	v_med3_f32 v14, v14, s54, v192
	v_med3_f32 v26, v26, s54, v192
	v_cvt_pk_fp8_f32 v9, v14, v26 op_sel:[0,0,1]
	ds_write_b128 v1, v[6:9] offset:34816
	v_mul_f32_e32 v6, 0x43800000, v103
	v_mul_f32_e32 v7, 0x43800000, v123
	v_med3_f32 v10, v6, s54, v192
	v_med3_f32 v7, v7, s54, v192
	v_mov_b32_e32 v6, v163
	v_cvt_pk_fp8_f32 v6, v10, v7
	v_mul_f32_e32 v8, 0x43800000, v131
	v_mul_f32_e32 v9, 0x43800000, v139
	v_med3_f32 v8, v8, s54, v192
	v_med3_f32 v9, v9, s54, v192
	v_cvt_pk_fp8_f32 v6, v8, v9 op_sel:[0,0,1]
	v_mul_f32_e32 v7, 0x43800000, v71
	v_mul_f32_e32 v8, 0x43800000, v79
	v_med3_f32 v14, v7, s54, v192
	v_med3_f32 v8, v8, s54, v192
	v_mov_b32_e32 v7, v163
	v_cvt_pk_fp8_f32 v7, v14, v8
	v_mul_f32_e32 v9, 0x43800000, v107
	v_mul_f32_e32 v10, 0x43800000, v127
	v_med3_f32 v9, v9, s54, v192
	v_med3_f32 v10, v10, s54, v192
	v_cvt_pk_fp8_f32 v7, v9, v10 op_sel:[0,0,1]
	v_mul_f32_e32 v8, 0x43800000, v35
	v_mul_f32_e32 v9, 0x43800000, v43
	v_med3_f32 v26, v8, s54, v192
	v_med3_f32 v9, v9, s54, v192
	v_mov_b32_e32 v8, v163
	v_cvt_pk_fp8_f32 v8, v26, v9
	v_mul_f32_e32 v10, 0x43800000, v75
	v_mul_f32_e32 v14, 0x43800000, v99
	v_med3_f32 v10, v10, s54, v192
	v_med3_f32 v14, v14, s54, v192
	v_cvt_pk_fp8_f32 v8, v10, v14 op_sel:[0,0,1]
	v_mul_f32_e32 v9, 0x43800000, v11
	v_mul_f32_e32 v10, 0x43800000, v15
	v_med3_f32 v15, v9, s54, v192
	v_med3_f32 v10, v10, s54, v192
	v_mov_b32_e32 v9, v163
	v_cvt_pk_fp8_f32 v9, v15, v10
	v_mul_f32_e32 v11, 0x43800000, v39
	v_mul_f32_e32 v14, 0x43800000, v67
	v_med3_f32 v11, v11, s54, v192
	v_med3_f32 v14, v14, s54, v192
	v_cvt_pk_fp8_f32 v9, v11, v14 op_sel:[0,0,1]
	ds_write_b128 v1, v[6:9] offset:35088
	v_mul_f32_e32 v6, 0x43800000, v104
	v_mul_f32_e32 v7, 0x43800000, v124
	v_med3_f32 v10, v6, s54, v192
	v_med3_f32 v7, v7, s54, v192
	v_mov_b32_e32 v6, v163
	v_cvt_pk_fp8_f32 v6, v10, v7
	v_mul_f32_e32 v8, 0x43800000, v132
	v_mul_f32_e32 v9, 0x43800000, v140
	v_med3_f32 v8, v8, s54, v192
	v_med3_f32 v9, v9, s54, v192
	v_cvt_pk_fp8_f32 v6, v8, v9 op_sel:[0,0,1]
	v_mul_f32_e32 v7, 0x43800000, v72
	v_mul_f32_e32 v8, 0x43800000, v80
	v_med3_f32 v11, v7, s54, v192
	v_med3_f32 v8, v8, s54, v192
	v_mov_b32_e32 v7, v163
	v_cvt_pk_fp8_f32 v7, v11, v8
	v_mul_f32_e32 v9, 0x43800000, v108
	v_mul_f32_e32 v10, 0x43800000, v128
	v_med3_f32 v9, v9, s54, v192
	v_med3_f32 v10, v10, s54, v192
	v_cvt_pk_fp8_f32 v7, v9, v10 op_sel:[0,0,1]
	v_mul_f32_e32 v8, 0x43800000, v36
	v_mul_f32_e32 v9, 0x43800000, v44
	v_med3_f32 v14, v8, s54, v192
	v_med3_f32 v9, v9, s54, v192
	v_mov_b32_e32 v8, v163
	v_cvt_pk_fp8_f32 v8, v14, v9
	v_mul_f32_e32 v10, 0x43800000, v76
	v_mul_f32_e32 v11, 0x43800000, v100
	v_med3_f32 v10, v10, s54, v192
	v_med3_f32 v11, v11, s54, v192
	v_cvt_pk_fp8_f32 v8, v10, v11 op_sel:[0,0,1]
	v_mul_f32_e32 v9, 0x43800000, v12
	v_mul_f32_e32 v10, 0x43800000, v16
	v_med3_f32 v14, v9, s54, v192
	v_med3_f32 v10, v10, s54, v192
	v_mov_b32_e32 v9, v163
	v_cvt_pk_fp8_f32 v9, v14, v10
	v_mul_f32_e32 v11, 0x43800000, v40
	v_mul_f32_e32 v12, 0x43800000, v68
	v_med3_f32 v11, v11, s54, v192
	v_med3_f32 v12, v12, s54, v192
	v_cvt_pk_fp8_f32 v9, v11, v12 op_sel:[0,0,1]
	ds_write_b128 v1, v[6:9] offset:35360
	v_mul_f32_e32 v6, 0x43800000, v105
	v_mul_f32_e32 v7, 0x43800000, v125
	v_med3_f32 v10, v6, s54, v192
	v_med3_f32 v7, v7, s54, v192
	v_mov_b32_e32 v6, v163
	v_cvt_pk_fp8_f32 v6, v10, v7
	v_mul_f32_e32 v8, 0x43800000, v133
	v_mul_f32_e32 v9, 0x43800000, v141
	v_med3_f32 v8, v8, s54, v192
	v_med3_f32 v9, v9, s54, v192
	v_cvt_pk_fp8_f32 v6, v8, v9 op_sel:[0,0,1]
	v_mul_f32_e32 v7, 0x43800000, v73
	v_mul_f32_e32 v8, 0x43800000, v81
	v_med3_f32 v11, v7, s54, v192
	v_med3_f32 v8, v8, s54, v192
	v_mov_b32_e32 v7, v163
	v_cvt_pk_fp8_f32 v7, v11, v8
	v_mul_f32_e32 v9, 0x43800000, v109
	v_mul_f32_e32 v10, 0x43800000, v129
	v_med3_f32 v9, v9, s54, v192
	v_med3_f32 v10, v10, s54, v192
	v_cvt_pk_fp8_f32 v7, v9, v10 op_sel:[0,0,1]
	v_mul_f32_e32 v8, 0x43800000, v37
	v_mul_f32_e32 v9, 0x43800000, v45
	v_med3_f32 v12, v8, s54, v192
	v_med3_f32 v9, v9, s54, v192
	v_mov_b32_e32 v8, v163
	v_cvt_pk_fp8_f32 v8, v12, v9
	v_mul_f32_e32 v10, 0x43800000, v77
	v_mul_f32_e32 v11, 0x43800000, v101
	v_med3_f32 v10, v10, s54, v192
	v_med3_f32 v11, v11, s54, v192
	v_cvt_pk_fp8_f32 v8, v10, v11 op_sel:[0,0,1]
	v_mul_f32_e32 v9, 0x43800000, v13
	v_mul_f32_e32 v10, 0x43800000, v17
	v_med3_f32 v13, v9, s54, v192
	v_med3_f32 v10, v10, s54, v192
	v_mov_b32_e32 v9, v163
	v_cvt_pk_fp8_f32 v9, v13, v10
	v_mul_f32_e32 v11, 0x43800000, v41
	v_mul_f32_e32 v12, 0x43800000, v69
	v_med3_f32 v11, v11, s54, v192
	v_med3_f32 v12, v12, s54, v192
	v_cvt_pk_fp8_f32 v9, v11, v12 op_sel:[0,0,1]
	ds_write_b128 v1, v[6:9] offset:35632
	s_waitcnt lgkmcnt(0)
	s_barrier
	s_mov_b32 s1, 0x1400000
	v_add_co_u32_e32 v6, vcc, s1, v164
	s_mov_b32 s1, 0x1404000
	s_nop 0
	v_addc_co_u32_e32 v7, vcc, 0, v165, vcc
	v_add_co_u32_e32 v8, vcc, s1, v164
	s_mov_b32 s1, 0x1408000
	s_nop 0
	v_addc_co_u32_e32 v9, vcc, 0, v165, vcc
	global_load_dwordx4 v[94:97], v[6:7], off sc0 nt
	global_load_dwordx4 v[102:105], v[8:9], off sc0 nt
	v_add_co_u32_e32 v6, vcc, s1, v164
	s_mov_b32 s1, 0x140c000
	s_nop 0
	v_addc_co_u32_e32 v7, vcc, 0, v165, vcc
	v_add_co_u32_e32 v8, vcc, s1, v164
	s_mov_b32 s1, 0x1410000
	s_nop 0
	v_addc_co_u32_e32 v9, vcc, 0, v165, vcc
	global_load_dwordx4 v[122:125], v[6:7], off sc0 nt
	global_load_dwordx4 v[126:129], v[8:9], off sc0 nt
	v_add_co_u32_e32 v6, vcc, s1, v164
	s_mov_b32 s1, 0x1414000
	s_nop 0
	v_addc_co_u32_e32 v7, vcc, 0, v165, vcc
	v_add_co_u32_e32 v8, vcc, s1, v164
	s_mov_b32 s1, 0x1418000
	s_nop 0
	v_addc_co_u32_e32 v9, vcc, 0, v165, vcc
	global_load_dwordx4 v[58:61], v[6:7], off sc0 nt
	global_load_dwordx4 v[70:73], v[8:9], off sc0 nt
	v_add_co_u32_e32 v6, vcc, s1, v164
	s_mov_b32 s1, 0x141c000
	s_nop 0
	v_addc_co_u32_e32 v7, vcc, 0, v165, vcc
	v_add_co_u32_e32 v8, vcc, s1, v164
	s_mov_b32 s1, 0x1420000
	s_nop 0
	v_addc_co_u32_e32 v9, vcc, 0, v165, vcc
	global_load_dwordx4 v[98:101], v[6:7], off sc0 nt
	global_load_dwordx4 v[106:109], v[8:9], off sc0 nt
	v_add_co_u32_e32 v6, vcc, s1, v164
	s_mov_b32 s1, 0x1424000
	s_nop 0
	v_addc_co_u32_e32 v7, vcc, 0, v165, vcc
	v_add_co_u32_e32 v8, vcc, s1, v164
	s_mov_b32 s1, 0x1428000
	s_nop 0
	v_addc_co_u32_e32 v9, vcc, 0, v165, vcc
	global_load_dwordx4 v[26:29], v[6:7], off sc0 nt
	global_load_dwordx4 v[38:41], v[8:9], off sc0 nt
	v_add_co_u32_e32 v6, vcc, s1, v164
	s_mov_b32 s1, 0x142c000
	s_nop 0
	v_addc_co_u32_e32 v7, vcc, 0, v165, vcc
	v_add_co_u32_e32 v8, vcc, s1, v164
	s_mov_b32 s1, 0x1430000
	s_nop 0
	v_addc_co_u32_e32 v9, vcc, 0, v165, vcc
	global_load_dwordx4 v[66:69], v[6:7], off sc0 nt
	global_load_dwordx4 v[74:77], v[8:9], off sc0 nt
	v_add_co_u32_e32 v6, vcc, s1, v164
	s_mov_b32 s1, 0x1434000
	s_nop 0
	v_addc_co_u32_e32 v7, vcc, 0, v165, vcc
	v_add_co_u32_e32 v10, vcc, s1, v164
	s_mov_b32 s1, 0x1438000
	s_nop 0
	v_addc_co_u32_e32 v11, vcc, 0, v165, vcc
	v_add_co_u32_e32 v14, vcc, s1, v164
	s_mov_b32 s1, 0x143c000
	s_nop 0
	v_addc_co_u32_e32 v15, vcc, 0, v165, vcc
	v_add_co_u32_e32 v16, vcc, s1, v164
	global_load_dwordx4 v[6:9], v[6:7], off sc0 nt
	s_nop 0
	global_load_dwordx4 v[10:13], v[10:11], off sc0 nt
	v_addc_co_u32_e32 v17, vcc, 0, v165, vcc
	global_load_dwordx4 v[34:37], v[14:15], off sc0 nt
	global_load_dwordx4 v[42:45], v[16:17], off sc0 nt
	ds_read_b128 v[14:17], v146 offset:34816
	s_waitcnt lgkmcnt(0)
	global_store_dwordx4 v[148:149], v[14:17], off offset:768 nt
	ds_read_b128 v[14:17], v150 offset:34816
	s_waitcnt lgkmcnt(0)
	global_store_dwordx4 v[152:153], v[14:17], off offset:768 nt
	ds_read_b128 v[14:17], v154 offset:34816
	s_waitcnt lgkmcnt(0)
	global_store_dwordx4 v[156:157], v[14:17], off offset:768 nt
	ds_read_b128 v[14:17], v158 offset:34816
	s_waitcnt lgkmcnt(0)
	global_store_dwordx4 v[160:161], v[14:17], off offset:768 nt
	s_waitcnt vmcnt(39)
	s_nop 0
	v_mul_f32_e32 v14, 0x43800000, v90
	s_waitcnt vmcnt(38)
	v_mul_f32_e32 v15, 0x43800000, v114
	v_med3_f32 v78, v14, s54, v192
	v_med3_f32 v15, v15, s54, v192
	v_mov_b32_e32 v14, v163
	v_cvt_pk_fp8_f32 v14, v78, v15
	s_waitcnt vmcnt(37)
	v_mul_f32_e32 v16, 0x43800000, v134
	s_waitcnt vmcnt(36)
	v_mul_f32_e32 v17, 0x43800000, v142
	v_med3_f32 v16, v16, s54, v192
	v_med3_f32 v17, v17, s54, v192
	v_cvt_pk_fp8_f32 v14, v16, v17 op_sel:[0,0,1]
	s_waitcnt vmcnt(35)
	v_mul_f32_e32 v15, 0x43800000, v54
	s_waitcnt vmcnt(34)
	v_mul_f32_e32 v16, 0x43800000, v82
	v_med3_f32 v78, v15, s54, v192
	v_med3_f32 v16, v16, s54, v192
	v_mov_b32_e32 v15, v163
	v_cvt_pk_fp8_f32 v15, v78, v16
	s_waitcnt vmcnt(33)
	v_mul_f32_e32 v17, 0x43800000, v110
	s_waitcnt vmcnt(32)
	v_mul_f32_e32 v54, 0x43800000, v118
	v_med3_f32 v17, v17, s54, v192
	v_med3_f32 v54, v54, s54, v192
	v_cvt_pk_fp8_f32 v15, v17, v54 op_sel:[0,0,1]
	s_waitcnt vmcnt(31)
	v_mul_f32_e32 v16, 0x43800000, v22
	s_waitcnt vmcnt(30)
	v_mul_f32_e32 v17, 0x43800000, v46
	v_med3_f32 v54, v16, s54, v192
	v_med3_f32 v17, v17, s54, v192
	v_mov_b32_e32 v16, v163
	v_cvt_pk_fp8_f32 v16, v54, v17
	s_waitcnt vmcnt(27)
	v_mul_f32_e32 v2, 0x43800000, v2
	s_waitcnt vmcnt(26)
	v_mul_f32_e32 v17, 0x43800000, v18
	s_waitcnt vmcnt(25)
	v_mul_f32_e32 v18, 0x43800000, v30
	v_med3_f32 v2, v2, s54, v192
	v_med3_f32 v30, v17, s54, v192
	v_mov_b32_e32 v17, v163
	v_mul_f32_e32 v22, 0x43800000, v62
	v_mul_f32_e32 v46, 0x43800000, v86
	v_cvt_pk_fp8_f32 v17, v2, v30
	v_med3_f32 v22, v22, s54, v192
	v_med3_f32 v46, v46, s54, v192
	v_cvt_pk_fp8_f32 v16, v22, v46 op_sel:[0,0,1]
	s_waitcnt vmcnt(24)
	v_mul_f32_e32 v22, 0x43800000, v50
	v_med3_f32 v18, v18, s54, v192
	v_med3_f32 v22, v22, s54, v192
	v_cvt_pk_fp8_f32 v17, v18, v22 op_sel:[0,0,1]
	v_mul_f32_e32 v2, 0x43800000, v91
	v_med3_f32 v2, v2, s54, v192
	v_mul_f32_e32 v5, 0x43800000, v5
	ds_write_b128 v1, v[14:17]
	v_mul_f32_e32 v14, 0x43800000, v115
	v_med3_f32 v17, v14, s54, v192
	v_mov_b32_e32 v14, v163
	v_cvt_pk_fp8_f32 v14, v2, v17
	v_mul_f32_e32 v15, 0x43800000, v135
	v_mul_f32_e32 v16, 0x43800000, v143
	v_med3_f32 v15, v15, s54, v192
	v_med3_f32 v16, v16, s54, v192
	v_cvt_pk_fp8_f32 v14, v15, v16 op_sel:[0,0,1]
	v_mul_f32_e32 v2, 0x43800000, v55
	v_mul_f32_e32 v15, 0x43800000, v83
	v_med3_f32 v2, v2, s54, v192
	v_med3_f32 v18, v15, s54, v192
	v_mov_b32_e32 v15, v163
	v_cvt_pk_fp8_f32 v15, v2, v18
	v_mul_f32_e32 v16, 0x43800000, v111
	v_mul_f32_e32 v17, 0x43800000, v119
	v_med3_f32 v16, v16, s54, v192
	v_med3_f32 v17, v17, s54, v192
	v_cvt_pk_fp8_f32 v15, v16, v17 op_sel:[0,0,1]
	v_mul_f32_e32 v2, 0x43800000, v23
	v_mul_f32_e32 v16, 0x43800000, v47
	v_med3_f32 v2, v2, s54, v192
	v_med3_f32 v22, v16, s54, v192
	v_mov_b32_e32 v16, v163
	v_cvt_pk_fp8_f32 v16, v2, v22
	v_mul_f32_e32 v17, 0x43800000, v63
	v_mul_f32_e32 v18, 0x43800000, v87
	v_med3_f32 v17, v17, s54, v192
	v_med3_f32 v18, v18, s54, v192
	v_cvt_pk_fp8_f32 v16, v17, v18 op_sel:[0,0,1]
	v_mul_f32_e32 v2, 0x43800000, v3
	v_mul_f32_e32 v3, 0x43800000, v19
	v_mul_f32_e32 v17, 0x43800000, v31
	v_med3_f32 v2, v2, s54, v192
	v_med3_f32 v3, v3, s54, v192
	v_med3_f32 v19, v17, s54, v192
	v_mov_b32_e32 v17, v163
	v_cvt_pk_fp8_f32 v17, v2, v3
	v_mul_f32_e32 v18, 0x43800000, v51
	v_med3_f32 v18, v18, s54, v192
	v_mul_f32_e32 v2, 0x43800000, v92
	v_cvt_pk_fp8_f32 v17, v19, v18 op_sel:[0,0,1]
	v_mul_f32_e32 v3, 0x43800000, v116
	v_med3_f32 v2, v2, s54, v192
	v_med3_f32 v3, v3, s54, v192
	ds_write_b128 v1, v[14:17] offset:272
	v_mul_f32_e32 v14, 0x43800000, v136
	v_med3_f32 v16, v14, s54, v192
	v_mov_b32_e32 v14, v163
	v_cvt_pk_fp8_f32 v14, v2, v3
	v_mul_f32_e32 v15, 0x43800000, v144
	v_med3_f32 v15, v15, s54, v192
	v_mul_f32_e32 v2, 0x43800000, v56
	v_cvt_pk_fp8_f32 v14, v16, v15 op_sel:[0,0,1]
	v_mul_f32_e32 v3, 0x43800000, v84
	v_mul_f32_e32 v15, 0x43800000, v112
	v_med3_f32 v2, v2, s54, v192
	v_med3_f32 v3, v3, s54, v192
	v_med3_f32 v17, v15, s54, v192
	v_mov_b32_e32 v15, v163
	v_cvt_pk_fp8_f32 v15, v2, v3
	v_mul_f32_e32 v16, 0x43800000, v120
	v_med3_f32 v16, v16, s54, v192
	v_mul_f32_e32 v2, 0x43800000, v24
	v_cvt_pk_fp8_f32 v15, v17, v16 op_sel:[0,0,1]
	v_mul_f32_e32 v3, 0x43800000, v48
	v_mul_f32_e32 v16, 0x43800000, v64
	v_med3_f32 v2, v2, s54, v192
	v_med3_f32 v3, v3, s54, v192
	v_med3_f32 v18, v16, s54, v192
	v_mov_b32_e32 v16, v163
	v_cvt_pk_fp8_f32 v16, v2, v3
	v_mul_f32_e32 v17, 0x43800000, v88
	v_med3_f32 v17, v17, s54, v192
	v_mul_f32_e32 v2, 0x43800000, v4
	v_cvt_pk_fp8_f32 v16, v18, v17 op_sel:[0,0,1]
	v_mul_f32_e32 v3, 0x43800000, v20
	v_mul_f32_e32 v17, 0x43800000, v52
	v_med3_f32 v2, v2, s54, v192
	v_med3_f32 v3, v3, s54, v192
	v_med3_f32 v18, v17, s54, v192
	v_mov_b32_e32 v17, v163
	v_cvt_pk_fp8_f32 v17, v2, v3
	v_mul_f32_e32 v4, 0x43800000, v32
	v_med3_f32 v4, v4, s54, v192
	v_mul_f32_e32 v2, 0x43800000, v93
	v_cvt_pk_fp8_f32 v17, v4, v18 op_sel:[0,0,1]
	v_mul_f32_e32 v3, 0x43800000, v117
	v_med3_f32 v3, v3, s54, v192
	v_mul_f32_e32 v4, 0x43800000, v137
	ds_write_b128 v1, v[14:17] offset:544
	v_med3_f32 v15, v2, s54, v192
	v_mov_b32_e32 v2, v163
	v_cvt_pk_fp8_f32 v2, v15, v3
	v_mul_f32_e32 v14, 0x43800000, v145
	v_med3_f32 v4, v4, s54, v192
	v_med3_f32 v14, v14, s54, v192
	v_cvt_pk_fp8_f32 v2, v4, v14 op_sel:[0,0,1]
	v_mul_f32_e32 v3, 0x43800000, v57
	v_mul_f32_e32 v4, 0x43800000, v85
	v_med3_f32 v16, v3, s54, v192
	v_med3_f32 v4, v4, s54, v192
	v_mov_b32_e32 v3, v163
	v_cvt_pk_fp8_f32 v3, v16, v4
	v_mul_f32_e32 v14, 0x43800000, v113
	v_mul_f32_e32 v15, 0x43800000, v121
	v_med3_f32 v14, v14, s54, v192
	v_med3_f32 v15, v15, s54, v192
	v_cvt_pk_fp8_f32 v3, v14, v15 op_sel:[0,0,1]
	v_mul_f32_e32 v4, 0x43800000, v25
	v_mul_f32_e32 v14, 0x43800000, v49
	v_med3_f32 v17, v4, s54, v192
	v_med3_f32 v14, v14, s54, v192
	v_mov_b32_e32 v4, v163
	v_cvt_pk_fp8_f32 v4, v17, v14
	v_mul_f32_e32 v14, 0x43800000, v21
	v_med3_f32 v17, v5, s54, v192
	v_med3_f32 v14, v14, s54, v192
	v_mov_b32_e32 v5, v163
	v_mul_f32_e32 v15, 0x43800000, v65
	v_mul_f32_e32 v16, 0x43800000, v89
	v_cvt_pk_fp8_f32 v5, v17, v14
	v_med3_f32 v15, v15, s54, v192
	v_med3_f32 v16, v16, s54, v192
	v_cvt_pk_fp8_f32 v4, v15, v16 op_sel:[0,0,1]
	v_mul_f32_e32 v15, 0x43800000, v33
	v_mul_f32_e32 v16, 0x43800000, v53
	v_med3_f32 v15, v15, s54, v192
	v_med3_f32 v16, v16, s54, v192
	v_cvt_pk_fp8_f32 v5, v15, v16 op_sel:[0,0,1]
	ds_write_b128 v1, v[2:5] offset:816
	s_waitcnt lgkmcnt(0)
	s_barrier
	s_mov_b32 s1, 0x1800000
	v_add_co_u32_e32 v2, vcc, s1, v164
	s_mov_b32 s1, 0x1804000
	s_nop 0
	v_addc_co_u32_e32 v3, vcc, 0, v165, vcc
	v_add_co_u32_e32 v4, vcc, s1, v164
	s_mov_b32 s1, 0x1808000
	s_nop 0
	v_addc_co_u32_e32 v5, vcc, 0, v165, vcc
	global_load_dwordx4 v[82:85], v[2:3], off sc0 nt
	global_load_dwordx4 v[90:93], v[4:5], off sc0 nt
	v_add_co_u32_e32 v2, vcc, s1, v164
	s_mov_b32 s1, 0x180c000
	s_nop 0
	v_addc_co_u32_e32 v3, vcc, 0, v165, vcc
	v_add_co_u32_e32 v4, vcc, s1, v164
	s_mov_b32 s1, 0x1810000
	s_nop 0
	v_addc_co_u32_e32 v5, vcc, 0, v165, vcc
	global_load_dwordx4 v[114:117], v[2:3], off sc0 nt
	global_load_dwordx4 v[118:121], v[4:5], off sc0 nt
	v_add_co_u32_e32 v2, vcc, s1, v164
	s_mov_b32 s1, 0x1814000
	s_nop 0
	v_addc_co_u32_e32 v3, vcc, 0, v165, vcc
	v_add_co_u32_e32 v4, vcc, s1, v164
	s_mov_b32 s1, 0x1818000
	s_nop 0
	v_addc_co_u32_e32 v5, vcc, 0, v165, vcc
	global_load_dwordx4 v[50:53], v[2:3], off sc0 nt
	global_load_dwordx4 v[62:65], v[4:5], off sc0 nt
	v_add_co_u32_e32 v2, vcc, s1, v164
	s_mov_b32 s1, 0x181c000
	s_nop 0
	v_addc_co_u32_e32 v3, vcc, 0, v165, vcc
	v_add_co_u32_e32 v4, vcc, s1, v164
	s_mov_b32 s1, 0x1820000
	s_nop 0
	v_addc_co_u32_e32 v5, vcc, 0, v165, vcc
	global_load_dwordx4 v[86:89], v[2:3], off sc0 nt
	global_load_dwordx4 v[110:113], v[4:5], off sc0 nt
	v_add_co_u32_e32 v2, vcc, s1, v164
	s_mov_b32 s1, 0x1824000
	s_nop 0
	v_addc_co_u32_e32 v3, vcc, 0, v165, vcc
	v_add_co_u32_e32 v4, vcc, s1, v164
	s_mov_b32 s1, 0x1828000
	s_nop 0
	v_addc_co_u32_e32 v5, vcc, 0, v165, vcc
	global_load_dwordx4 v[18:21], v[2:3], off sc0 nt
	global_load_dwordx4 v[30:33], v[4:5], off sc0 nt
	v_add_co_u32_e32 v2, vcc, s1, v164
	s_mov_b32 s1, 0x182c000
	s_nop 0
	v_addc_co_u32_e32 v3, vcc, 0, v165, vcc
	v_add_co_u32_e32 v4, vcc, s1, v164
	s_mov_b32 s1, 0x1830000
	s_nop 0
	v_addc_co_u32_e32 v5, vcc, 0, v165, vcc
	global_load_dwordx4 v[54:57], v[2:3], off sc0 nt
	global_load_dwordx4 v[78:81], v[4:5], off sc0 nt
	v_add_co_u32_e32 v2, vcc, s1, v164
	s_mov_b32 s1, 0x1834000
	s_nop 0
	v_addc_co_u32_e32 v3, vcc, 0, v165, vcc
	v_add_co_u32_e32 v14, vcc, s1, v164
	s_mov_b32 s1, 0x1838000
	s_nop 0
	v_addc_co_u32_e32 v15, vcc, 0, v165, vcc
	v_add_co_u32_e32 v22, vcc, s1, v164
	s_mov_b32 s1, 0x183c000
	s_nop 0
	v_addc_co_u32_e32 v23, vcc, 0, v165, vcc
	v_add_co_u32_e32 v46, vcc, s1, v164
	global_load_dwordx4 v[2:5], v[2:3], off sc0 nt
	s_nop 0
	global_load_dwordx4 v[14:17], v[14:15], off sc0 nt
	v_addc_co_u32_e32 v47, vcc, 0, v165, vcc
	global_load_dwordx4 v[22:25], v[22:23], off sc0 nt
	s_nop 0
	global_load_dwordx4 v[46:49], v[46:47], off sc0 nt
	ds_read_b128 v[130:133], v146
	s_waitcnt lgkmcnt(0)
	global_store_dwordx4 v[148:149], v[130:133], off offset:1024 nt
	ds_read_b128 v[130:133], v150
	s_waitcnt lgkmcnt(0)
	global_store_dwordx4 v[152:153], v[130:133], off offset:1024 nt
	ds_read_b128 v[130:133], v154
	s_waitcnt lgkmcnt(0)
	global_store_dwordx4 v[156:157], v[130:133], off offset:1024 nt
	ds_read_b128 v[130:133], v158
	s_waitcnt lgkmcnt(0)
	global_store_dwordx4 v[160:161], v[130:133], off offset:1024 nt
	s_waitcnt vmcnt(39)
	v_mul_f32_e32 v94, 0x43800000, v94
	s_waitcnt vmcnt(38)
	v_mul_f32_e32 v102, 0x43800000, v102
	s_waitcnt vmcnt(35)
	v_mul_f32_e32 v58, 0x43800000, v58
	s_waitcnt vmcnt(34)
	v_mul_f32_e32 v70, 0x43800000, v70
	s_waitcnt vmcnt(31)
	v_mul_f32_e32 v26, 0x43800000, v26
	s_waitcnt vmcnt(30)
	v_mul_f32_e32 v38, 0x43800000, v38
	s_waitcnt vmcnt(27)
	v_mul_f32_e32 v6, 0x43800000, v6
	s_waitcnt vmcnt(26)
	v_mul_f32_e32 v10, 0x43800000, v10
	v_med3_f32 v94, v94, s54, v192
	v_med3_f32 v102, v102, s54, v192
	v_mov_b32_e32 v130, v163
	v_med3_f32 v58, v58, s54, v192
	v_med3_f32 v70, v70, s54, v192
	v_mov_b32_e32 v131, v163
	v_med3_f32 v26, v26, s54, v192
	v_med3_f32 v38, v38, s54, v192
	v_mov_b32_e32 v132, v163
	v_med3_f32 v6, v6, s54, v192
	v_med3_f32 v10, v10, s54, v192
	v_mov_b32_e32 v133, v163
	v_cvt_pk_fp8_f32 v130, v94, v102
	v_cvt_pk_fp8_f32 v131, v58, v70
	v_cvt_pk_fp8_f32 v132, v26, v38
	v_cvt_pk_fp8_f32 v133, v6, v10
	v_mul_f32_e32 v122, 0x43800000, v122
	v_mul_f32_e32 v126, 0x43800000, v126
	v_mul_f32_e32 v94, 0x43800000, v98
	v_mul_f32_e32 v98, 0x43800000, v106
	v_mul_f32_e32 v58, 0x43800000, v66
	v_mul_f32_e32 v66, 0x43800000, v74
	s_waitcnt vmcnt(25)
	v_mul_f32_e32 v26, 0x43800000, v34
	s_waitcnt vmcnt(24)
	v_mul_f32_e32 v34, 0x43800000, v42
	v_med3_f32 v122, v122, s54, v192
	v_med3_f32 v126, v126, s54, v192
	v_med3_f32 v94, v94, s54, v192
	v_med3_f32 v98, v98, s54, v192
	v_med3_f32 v58, v58, s54, v192
	v_med3_f32 v66, v66, s54, v192
	v_med3_f32 v26, v26, s54, v192
	v_med3_f32 v34, v34, s54, v192
	v_cvt_pk_fp8_f32 v130, v122, v126 op_sel:[0,0,1]
	v_cvt_pk_fp8_f32 v131, v94, v98 op_sel:[0,0,1]
	v_cvt_pk_fp8_f32 v132, v58, v66 op_sel:[0,0,1]
	v_cvt_pk_fp8_f32 v133, v26, v34 op_sel:[0,0,1]
	v_mul_f32_e32 v6, 0x43800000, v95
	v_mul_f32_e32 v10, 0x43800000, v103
	v_med3_f32 v6, v6, s54, v192
	ds_write_b128 v1, v[130:133] offset:34816
	v_med3_f32 v10, v10, s54, v192
	v_mov_b32_e32 v130, v163
	v_cvt_pk_fp8_f32 v130, v6, v10
	v_mul_f32_e32 v6, 0x43800000, v59
	v_mul_f32_e32 v10, 0x43800000, v71
	v_med3_f32 v6, v6, s54, v192
	v_med3_f32 v10, v10, s54, v192
	v_mov_b32_e32 v131, v163
	v_cvt_pk_fp8_f32 v131, v6, v10
	v_mul_f32_e32 v6, 0x43800000, v27
	v_mul_f32_e32 v10, 0x43800000, v39
	v_med3_f32 v6, v6, s54, v192
	v_med3_f32 v10, v10, s54, v192
	v_mov_b32_e32 v132, v163
	v_mul_f32_e32 v26, 0x43800000, v123
	v_mul_f32_e32 v34, 0x43800000, v127
	v_cvt_pk_fp8_f32 v132, v6, v10
	v_mul_f32_e32 v6, 0x43800000, v7
	v_mul_f32_e32 v7, 0x43800000, v11
	v_med3_f32 v26, v26, s54, v192
	v_med3_f32 v34, v34, s54, v192
	v_med3_f32 v6, v6, s54, v192
	v_med3_f32 v7, v7, s54, v192
	v_mov_b32_e32 v133, v163
	v_cvt_pk_fp8_f32 v130, v26, v34 op_sel:[0,0,1]
	v_mul_f32_e32 v26, 0x43800000, v99
	v_mul_f32_e32 v34, 0x43800000, v107
	v_cvt_pk_fp8_f32 v133, v6, v7
	v_med3_f32 v26, v26, s54, v192
	v_med3_f32 v34, v34, s54, v192
	v_cvt_pk_fp8_f32 v131, v26, v34 op_sel:[0,0,1]
	v_mul_f32_e32 v26, 0x43800000, v67
	v_mul_f32_e32 v27, 0x43800000, v75
	v_mul_f32_e32 v10, 0x43800000, v35
	v_mul_f32_e32 v11, 0x43800000, v43
	v_med3_f32 v26, v26, s54, v192
	v_med3_f32 v27, v27, s54, v192
	v_med3_f32 v10, v10, s54, v192
	v_med3_f32 v11, v11, s54, v192
	v_cvt_pk_fp8_f32 v132, v26, v27 op_sel:[0,0,1]
	v_cvt_pk_fp8_f32 v133, v10, v11 op_sel:[0,0,1]
	v_mul_f32_e32 v6, 0x43800000, v96
	v_mul_f32_e32 v7, 0x43800000, v104
	v_med3_f32 v6, v6, s54, v192
	ds_write_b128 v1, v[130:133] offset:35088
	v_med3_f32 v7, v7, s54, v192
	v_mov_b32_e32 v130, v163
	v_cvt_pk_fp8_f32 v130, v6, v7
	v_mul_f32_e32 v6, 0x43800000, v60
	v_mul_f32_e32 v7, 0x43800000, v72
	v_med3_f32 v6, v6, s54, v192
	v_med3_f32 v7, v7, s54, v192
	v_mov_b32_e32 v131, v163
	v_mul_f32_e32 v10, 0x43800000, v124
	v_mul_f32_e32 v11, 0x43800000, v128
	v_cvt_pk_fp8_f32 v131, v6, v7
	v_mul_f32_e32 v6, 0x43800000, v28
	v_mul_f32_e32 v7, 0x43800000, v40
	v_med3_f32 v10, v10, s54, v192
	v_med3_f32 v11, v11, s54, v192
	v_med3_f32 v6, v6, s54, v192
	v_med3_f32 v7, v7, s54, v192
	v_mov_b32_e32 v132, v163
	v_cvt_pk_fp8_f32 v130, v10, v11 op_sel:[0,0,1]
	v_mul_f32_e32 v10, 0x43800000, v100
	v_mul_f32_e32 v11, 0x43800000, v108
	v_cvt_pk_fp8_f32 v132, v6, v7
	v_med3_f32 v10, v10, s54, v192
	v_med3_f32 v11, v11, s54, v192
	v_mul_f32_e32 v6, 0x43800000, v8
	v_mul_f32_e32 v7, 0x43800000, v12
	v_cvt_pk_fp8_f32 v131, v10, v11 op_sel:[0,0,1]
	v_mul_f32_e32 v10, 0x43800000, v68
	v_mul_f32_e32 v11, 0x43800000, v76
	v_med3_f32 v6, v6, s54, v192
	v_med3_f32 v7, v7, s54, v192
	v_mov_b32_e32 v133, v163
	v_med3_f32 v10, v10, s54, v192
	v_med3_f32 v11, v11, s54, v192
	v_cvt_pk_fp8_f32 v133, v6, v7
	v_mul_f32_e32 v6, 0x43800000, v97
	v_mul_f32_e32 v7, 0x43800000, v105
	v_cvt_pk_fp8_f32 v132, v10, v11 op_sel:[0,0,1]
	v_med3_f32 v11, v6, s54, v192
	v_med3_f32 v7, v7, s54, v192
	v_mov_b32_e32 v6, v163
	v_mul_f32_e32 v8, 0x43800000, v36
	v_mul_f32_e32 v10, 0x43800000, v44
	v_cvt_pk_fp8_f32 v6, v11, v7
	v_med3_f32 v8, v8, s54, v192
	v_med3_f32 v10, v10, s54, v192
	v_cvt_pk_fp8_f32 v133, v8, v10 op_sel:[0,0,1]
	v_mul_f32_e32 v8, 0x43800000, v125
	v_mul_f32_e32 v10, 0x43800000, v129
	v_med3_f32 v8, v8, s54, v192
	v_med3_f32 v10, v10, s54, v192
	v_cvt_pk_fp8_f32 v6, v8, v10 op_sel:[0,0,1]
	v_mul_f32_e32 v7, 0x43800000, v61
	v_mul_f32_e32 v8, 0x43800000, v73
	v_med3_f32 v12, v7, s54, v192
	v_med3_f32 v8, v8, s54, v192
	v_mov_b32_e32 v7, v163
	v_cvt_pk_fp8_f32 v7, v12, v8
	v_mul_f32_e32 v10, 0x43800000, v101
	v_mul_f32_e32 v11, 0x43800000, v109
	v_med3_f32 v10, v10, s54, v192
	v_med3_f32 v11, v11, s54, v192
	v_cvt_pk_fp8_f32 v7, v10, v11 op_sel:[0,0,1]
	v_mul_f32_e32 v8, 0x43800000, v29
	v_mul_f32_e32 v10, 0x43800000, v41
	v_med3_f32 v26, v8, s54, v192
	v_med3_f32 v10, v10, s54, v192
	v_mov_b32_e32 v8, v163
	v_cvt_pk_fp8_f32 v8, v26, v10
	v_mul_f32_e32 v9, 0x43800000, v9
	v_mul_f32_e32 v10, 0x43800000, v13
	v_med3_f32 v13, v9, s54, v192
	v_med3_f32 v10, v10, s54, v192
	v_mov_b32_e32 v9, v163
	v_mul_f32_e32 v11, 0x43800000, v69
	v_mul_f32_e32 v12, 0x43800000, v77
	v_cvt_pk_fp8_f32 v9, v13, v10
	v_med3_f32 v11, v11, s54, v192
	v_med3_f32 v12, v12, s54, v192
	v_cvt_pk_fp8_f32 v8, v11, v12 op_sel:[0,0,1]
	v_mul_f32_e32 v11, 0x43800000, v37
	v_mul_f32_e32 v12, 0x43800000, v45
	v_med3_f32 v11, v11, s54, v192
	v_med3_f32 v12, v12, s54, v192
	v_cvt_pk_fp8_f32 v9, v11, v12 op_sel:[0,0,1]
	ds_write_b128 v1, v[130:133] offset:35360
	ds_write_b128 v1, v[6:9] offset:35632
	s_waitcnt lgkmcnt(0)
	s_barrier
	s_mov_b32 s1, 0x1c00000
	v_add_co_u32_e32 v6, vcc, s1, v164
	s_mov_b32 s1, 0x1c04000
	s_nop 0
	v_addc_co_u32_e32 v7, vcc, 0, v165, vcc
	v_add_co_u32_e32 v8, vcc, s1, v164
	s_mov_b32 s1, 0x1c08000
	s_nop 0
	v_addc_co_u32_e32 v9, vcc, 0, v165, vcc
	global_load_dwordx4 v[94:97], v[6:7], off sc0 nt
	global_load_dwordx4 v[102:105], v[8:9], off sc0 nt
	v_add_co_u32_e32 v6, vcc, s1, v164
	s_mov_b32 s1, 0x1c0c000
	s_nop 0
	v_addc_co_u32_e32 v7, vcc, 0, v165, vcc
	v_add_co_u32_e32 v8, vcc, s1, v164
	s_mov_b32 s1, 0x1c10000
	s_nop 0
	v_addc_co_u32_e32 v9, vcc, 0, v165, vcc
	global_load_dwordx4 v[122:125], v[6:7], off sc0 nt
	global_load_dwordx4 v[126:129], v[8:9], off sc0 nt
	v_add_co_u32_e32 v6, vcc, s1, v164
	s_mov_b32 s1, 0x1c14000
	s_nop 0
	v_addc_co_u32_e32 v7, vcc, 0, v165, vcc
	v_add_co_u32_e32 v8, vcc, s1, v164
	s_mov_b32 s1, 0x1c18000
	s_nop 0
	v_addc_co_u32_e32 v9, vcc, 0, v165, vcc
	global_load_dwordx4 v[58:61], v[6:7], off sc0 nt
	global_load_dwordx4 v[70:73], v[8:9], off sc0 nt
	v_add_co_u32_e32 v6, vcc, s1, v164
	s_mov_b32 s1, 0x1c1c000
	s_nop 0
	v_addc_co_u32_e32 v7, vcc, 0, v165, vcc
	v_add_co_u32_e32 v8, vcc, s1, v164
	s_mov_b32 s1, 0x1c20000
	s_nop 0
	v_addc_co_u32_e32 v9, vcc, 0, v165, vcc
	global_load_dwordx4 v[98:101], v[6:7], off sc0 nt
	global_load_dwordx4 v[106:109], v[8:9], off sc0 nt
	v_add_co_u32_e32 v6, vcc, s1, v164
	s_mov_b32 s1, 0x1c24000
	s_nop 0
	v_addc_co_u32_e32 v7, vcc, 0, v165, vcc
	v_add_co_u32_e32 v8, vcc, s1, v164
	s_mov_b32 s1, 0x1c28000
	s_nop 0
	v_addc_co_u32_e32 v9, vcc, 0, v165, vcc
	global_load_dwordx4 v[26:29], v[6:7], off sc0 nt
	global_load_dwordx4 v[38:41], v[8:9], off sc0 nt
	v_add_co_u32_e32 v6, vcc, s1, v164
	s_mov_b32 s1, 0x1c2c000
	s_nop 0
	v_addc_co_u32_e32 v7, vcc, 0, v165, vcc
	v_add_co_u32_e32 v8, vcc, s1, v164
	s_mov_b32 s1, 0x1c30000
	s_nop 0
	v_addc_co_u32_e32 v9, vcc, 0, v165, vcc
	global_load_dwordx4 v[66:69], v[6:7], off sc0 nt
	global_load_dwordx4 v[74:77], v[8:9], off sc0 nt
	v_add_co_u32_e32 v6, vcc, s1, v164
	s_mov_b32 s1, 0x1c34000
	s_nop 0
	v_addc_co_u32_e32 v7, vcc, 0, v165, vcc
	v_add_co_u32_e32 v10, vcc, s1, v164
	s_mov_b32 s1, 0x1c38000
	s_nop 0
	v_addc_co_u32_e32 v11, vcc, 0, v165, vcc
	v_add_co_u32_e32 v34, vcc, s1, v164
	s_mov_b32 s1, 0x1c3c000
	s_nop 0
	v_addc_co_u32_e32 v35, vcc, 0, v165, vcc
	v_add_co_u32_e32 v42, vcc, s1, v164
	global_load_dwordx4 v[6:9], v[6:7], off sc0 nt
	s_nop 0
	global_load_dwordx4 v[10:13], v[10:11], off sc0 nt
	v_addc_co_u32_e32 v43, vcc, 0, v165, vcc
	global_load_dwordx4 v[34:37], v[34:35], off sc0 nt
	s_nop 0
	global_load_dwordx4 v[42:45], v[42:43], off sc0 nt
	ds_read_b128 v[130:133], v146 offset:34816
	s_waitcnt lgkmcnt(0)
	global_store_dwordx4 v[148:149], v[130:133], off offset:1280 nt
	ds_read_b128 v[130:133], v150 offset:34816
	s_waitcnt lgkmcnt(0)
	global_store_dwordx4 v[152:153], v[130:133], off offset:1280 nt
	ds_read_b128 v[130:133], v154 offset:34816
	s_waitcnt lgkmcnt(0)
	global_store_dwordx4 v[156:157], v[130:133], off offset:1280 nt
	ds_read_b128 v[130:133], v158 offset:34816
	s_waitcnt lgkmcnt(0)
	global_store_dwordx4 v[160:161], v[130:133], off offset:1280 nt
	s_waitcnt vmcnt(39)
	v_mul_f32_e32 v82, 0x43800000, v82
	s_waitcnt vmcnt(38)
	v_mul_f32_e32 v90, 0x43800000, v90
	s_waitcnt vmcnt(35)
	v_mul_f32_e32 v50, 0x43800000, v50
	s_waitcnt vmcnt(34)
	v_mul_f32_e32 v62, 0x43800000, v62
	s_waitcnt vmcnt(31)
	v_mul_f32_e32 v18, 0x43800000, v18
	s_waitcnt vmcnt(30)
	v_mul_f32_e32 v30, 0x43800000, v30
	s_waitcnt vmcnt(27)
	v_mul_f32_e32 v2, 0x43800000, v2
	s_waitcnt vmcnt(26)
	v_mul_f32_e32 v14, 0x43800000, v14
	v_med3_f32 v82, v82, s54, v192
	v_med3_f32 v90, v90, s54, v192
	v_mov_b32_e32 v130, v163
	v_med3_f32 v50, v50, s54, v192
	v_med3_f32 v62, v62, s54, v192
	v_mov_b32_e32 v131, v163
	v_med3_f32 v18, v18, s54, v192
	v_med3_f32 v30, v30, s54, v192
	v_mov_b32_e32 v132, v163
	v_med3_f32 v2, v2, s54, v192
	v_med3_f32 v14, v14, s54, v192
	v_mov_b32_e32 v133, v163
	v_cvt_pk_fp8_f32 v130, v82, v90
	v_cvt_pk_fp8_f32 v131, v50, v62
	v_cvt_pk_fp8_f32 v132, v18, v30
	v_cvt_pk_fp8_f32 v133, v2, v14
	v_mul_f32_e32 v114, 0x43800000, v114
	v_mul_f32_e32 v118, 0x43800000, v118
	v_mul_f32_e32 v82, 0x43800000, v86
	v_mul_f32_e32 v86, 0x43800000, v110
	v_mul_f32_e32 v50, 0x43800000, v54
	v_mul_f32_e32 v54, 0x43800000, v78
	s_waitcnt vmcnt(25)
	v_mul_f32_e32 v18, 0x43800000, v22
	s_waitcnt vmcnt(24)
	v_mul_f32_e32 v22, 0x43800000, v46
	v_med3_f32 v114, v114, s54, v192
	v_med3_f32 v118, v118, s54, v192
	v_med3_f32 v82, v82, s54, v192
	v_med3_f32 v86, v86, s54, v192
	v_med3_f32 v50, v50, s54, v192
	v_med3_f32 v54, v54, s54, v192
	v_med3_f32 v18, v18, s54, v192
	v_med3_f32 v22, v22, s54, v192
	v_cvt_pk_fp8_f32 v130, v114, v118 op_sel:[0,0,1]
	v_cvt_pk_fp8_f32 v131, v82, v86 op_sel:[0,0,1]
	v_cvt_pk_fp8_f32 v132, v50, v54 op_sel:[0,0,1]
	v_cvt_pk_fp8_f32 v133, v18, v22 op_sel:[0,0,1]
	v_mul_f32_e32 v2, 0x43800000, v83
	v_mul_f32_e32 v14, 0x43800000, v91
	v_med3_f32 v2, v2, s54, v192
	ds_write_b128 v1, v[130:133]
	v_med3_f32 v14, v14, s54, v192
	v_mov_b32_e32 v130, v163
	v_cvt_pk_fp8_f32 v130, v2, v14
	v_mul_f32_e32 v2, 0x43800000, v51
	v_mul_f32_e32 v14, 0x43800000, v63
	v_med3_f32 v2, v2, s54, v192
	v_med3_f32 v14, v14, s54, v192
	v_mov_b32_e32 v131, v163
	v_cvt_pk_fp8_f32 v131, v2, v14
	v_mul_f32_e32 v2, 0x43800000, v19
	v_mul_f32_e32 v14, 0x43800000, v31
	v_med3_f32 v2, v2, s54, v192
	v_med3_f32 v14, v14, s54, v192
	v_mov_b32_e32 v132, v163
	v_mul_f32_e32 v18, 0x43800000, v115
	v_mul_f32_e32 v22, 0x43800000, v119
	v_cvt_pk_fp8_f32 v132, v2, v14
	v_mul_f32_e32 v2, 0x43800000, v3
	v_mul_f32_e32 v3, 0x43800000, v15
	v_med3_f32 v18, v18, s54, v192
	v_med3_f32 v22, v22, s54, v192
	v_med3_f32 v2, v2, s54, v192
	v_med3_f32 v3, v3, s54, v192
	v_mov_b32_e32 v133, v163
	v_cvt_pk_fp8_f32 v130, v18, v22 op_sel:[0,0,1]
	v_mul_f32_e32 v18, 0x43800000, v87
	v_mul_f32_e32 v22, 0x43800000, v111
	v_cvt_pk_fp8_f32 v133, v2, v3
	v_med3_f32 v18, v18, s54, v192
	v_med3_f32 v22, v22, s54, v192
	v_cvt_pk_fp8_f32 v131, v18, v22 op_sel:[0,0,1]
	v_mul_f32_e32 v18, 0x43800000, v55
	v_mul_f32_e32 v19, 0x43800000, v79
	v_mul_f32_e32 v14, 0x43800000, v23
	v_mul_f32_e32 v15, 0x43800000, v47
	v_med3_f32 v18, v18, s54, v192
	v_med3_f32 v19, v19, s54, v192
	v_med3_f32 v14, v14, s54, v192
	v_med3_f32 v15, v15, s54, v192
	v_cvt_pk_fp8_f32 v132, v18, v19 op_sel:[0,0,1]
	v_cvt_pk_fp8_f32 v133, v14, v15 op_sel:[0,0,1]
	v_mul_f32_e32 v2, 0x43800000, v84
	v_mul_f32_e32 v3, 0x43800000, v92
	v_med3_f32 v2, v2, s54, v192
	ds_write_b128 v1, v[130:133] offset:272
	v_med3_f32 v3, v3, s54, v192
	v_mov_b32_e32 v130, v163
	v_cvt_pk_fp8_f32 v130, v2, v3
	v_mul_f32_e32 v2, 0x43800000, v52
	v_mul_f32_e32 v3, 0x43800000, v64
	v_med3_f32 v2, v2, s54, v192
	v_med3_f32 v3, v3, s54, v192
	v_mov_b32_e32 v131, v163
	v_mul_f32_e32 v14, 0x43800000, v116
	v_mul_f32_e32 v15, 0x43800000, v120
	v_cvt_pk_fp8_f32 v131, v2, v3
	v_mul_f32_e32 v2, 0x43800000, v20
	v_mul_f32_e32 v3, 0x43800000, v32
	v_med3_f32 v14, v14, s54, v192
	v_med3_f32 v15, v15, s54, v192
	v_med3_f32 v2, v2, s54, v192
	v_med3_f32 v3, v3, s54, v192
	v_mov_b32_e32 v132, v163
	v_cvt_pk_fp8_f32 v130, v14, v15 op_sel:[0,0,1]
	v_mul_f32_e32 v14, 0x43800000, v88
	v_mul_f32_e32 v15, 0x43800000, v112
	v_cvt_pk_fp8_f32 v132, v2, v3
	v_med3_f32 v14, v14, s54, v192
	v_med3_f32 v15, v15, s54, v192
	v_mul_f32_e32 v2, 0x43800000, v4
	v_mul_f32_e32 v3, 0x43800000, v16
	v_cvt_pk_fp8_f32 v131, v14, v15 op_sel:[0,0,1]
	v_mul_f32_e32 v14, 0x43800000, v56
	v_mul_f32_e32 v15, 0x43800000, v80
	v_med3_f32 v2, v2, s54, v192
	v_med3_f32 v3, v3, s54, v192
	v_mov_b32_e32 v133, v163
	v_med3_f32 v14, v14, s54, v192
	v_med3_f32 v15, v15, s54, v192
	v_cvt_pk_fp8_f32 v133, v2, v3
	v_mul_f32_e32 v2, 0x43800000, v85
	v_mul_f32_e32 v3, 0x43800000, v93
	v_cvt_pk_fp8_f32 v132, v14, v15 op_sel:[0,0,1]
	v_med3_f32 v15, v2, s54, v192
	v_med3_f32 v3, v3, s54, v192
	v_mov_b32_e32 v2, v163
	v_mul_f32_e32 v4, 0x43800000, v24
	v_mul_f32_e32 v14, 0x43800000, v48
	v_cvt_pk_fp8_f32 v2, v15, v3
	v_med3_f32 v4, v4, s54, v192
	v_med3_f32 v14, v14, s54, v192
	v_cvt_pk_fp8_f32 v133, v4, v14 op_sel:[0,0,1]
	v_mul_f32_e32 v4, 0x43800000, v117
	v_mul_f32_e32 v14, 0x43800000, v121
	v_med3_f32 v4, v4, s54, v192
	v_med3_f32 v14, v14, s54, v192
	v_cvt_pk_fp8_f32 v2, v4, v14 op_sel:[0,0,1]
	v_mul_f32_e32 v3, 0x43800000, v53
	v_mul_f32_e32 v4, 0x43800000, v65
	v_med3_f32 v16, v3, s54, v192
	v_med3_f32 v4, v4, s54, v192
	v_mov_b32_e32 v3, v163
	v_cvt_pk_fp8_f32 v3, v16, v4
	v_mul_f32_e32 v14, 0x43800000, v89
	v_mul_f32_e32 v15, 0x43800000, v113
	v_med3_f32 v14, v14, s54, v192
	v_med3_f32 v15, v15, s54, v192
	v_cvt_pk_fp8_f32 v3, v14, v15 op_sel:[0,0,1]
	v_mul_f32_e32 v4, 0x43800000, v21
	v_mul_f32_e32 v14, 0x43800000, v33
	v_med3_f32 v18, v4, s54, v192
	v_med3_f32 v14, v14, s54, v192
	v_mov_b32_e32 v4, v163
	v_cvt_pk_fp8_f32 v4, v18, v14
	v_mul_f32_e32 v5, 0x43800000, v5
	v_mul_f32_e32 v14, 0x43800000, v17
	v_med3_f32 v17, v5, s54, v192
	v_med3_f32 v14, v14, s54, v192
	v_mov_b32_e32 v5, v163
	v_mul_f32_e32 v15, 0x43800000, v57
	v_mul_f32_e32 v16, 0x43800000, v81
	v_cvt_pk_fp8_f32 v5, v17, v14
	v_med3_f32 v15, v15, s54, v192
	v_med3_f32 v16, v16, s54, v192
	v_cvt_pk_fp8_f32 v4, v15, v16 op_sel:[0,0,1]
	v_mul_f32_e32 v15, 0x43800000, v25
	v_mul_f32_e32 v16, 0x43800000, v49
	v_med3_f32 v15, v15, s54, v192
	v_med3_f32 v16, v16, s54, v192
	v_cvt_pk_fp8_f32 v5, v15, v16 op_sel:[0,0,1]
	ds_write_b128 v1, v[130:133] offset:544
	ds_write_b128 v1, v[2:5] offset:816
	s_waitcnt lgkmcnt(0)
	s_barrier
	ds_read_b128 v[2:5], v146
	s_waitcnt lgkmcnt(0)
	global_store_dwordx4 v[148:149], v[2:5], off offset:1536 nt
	ds_read_b128 v[2:5], v150
	s_waitcnt lgkmcnt(0)
	global_store_dwordx4 v[152:153], v[2:5], off offset:1536 nt
	ds_read_b128 v[2:5], v154
	s_waitcnt lgkmcnt(0)
	global_store_dwordx4 v[156:157], v[2:5], off offset:1536 nt
	ds_read_b128 v[2:5], v158
	s_waitcnt lgkmcnt(0)
	global_store_dwordx4 v[160:161], v[2:5], off offset:1536 nt
	s_waitcnt vmcnt(23)
	s_nop 0
	v_mul_f32_e32 v2, 0x43800000, v94
	s_waitcnt vmcnt(22)
	v_mul_f32_e32 v3, 0x43800000, v102
	v_med3_f32 v14, v2, s54, v192
	v_med3_f32 v3, v3, s54, v192
	v_mov_b32_e32 v2, v163
	v_cvt_pk_fp8_f32 v2, v14, v3
	s_waitcnt vmcnt(21)
	v_mul_f32_e32 v4, 0x43800000, v122
	s_waitcnt vmcnt(20)
	v_mul_f32_e32 v5, 0x43800000, v126
	v_med3_f32 v4, v4, s54, v192
	v_med3_f32 v5, v5, s54, v192
	v_cvt_pk_fp8_f32 v2, v4, v5 op_sel:[0,0,1]
	s_waitcnt vmcnt(19)
	v_mul_f32_e32 v3, 0x43800000, v58
	s_waitcnt vmcnt(18)
	v_mul_f32_e32 v4, 0x43800000, v70
	v_med3_f32 v15, v3, s54, v192
	v_med3_f32 v4, v4, s54, v192
	v_mov_b32_e32 v3, v163
	v_cvt_pk_fp8_f32 v3, v15, v4
	s_waitcnt vmcnt(17)
	v_mul_f32_e32 v5, 0x43800000, v98
	s_waitcnt vmcnt(16)
	v_mul_f32_e32 v14, 0x43800000, v106
	v_med3_f32 v5, v5, s54, v192
	v_med3_f32 v14, v14, s54, v192
	v_cvt_pk_fp8_f32 v3, v5, v14 op_sel:[0,0,1]
	s_waitcnt vmcnt(15)
	v_mul_f32_e32 v4, 0x43800000, v26
	s_waitcnt vmcnt(14)
	v_mul_f32_e32 v5, 0x43800000, v38
	v_med3_f32 v16, v4, s54, v192
	v_med3_f32 v5, v5, s54, v192
	v_mov_b32_e32 v4, v163
	v_cvt_pk_fp8_f32 v4, v16, v5
	s_waitcnt vmcnt(13)
	v_mul_f32_e32 v14, 0x43800000, v66
	s_waitcnt vmcnt(12)
	v_mul_f32_e32 v15, 0x43800000, v74
	v_med3_f32 v14, v14, s54, v192
	v_med3_f32 v15, v15, s54, v192
	s_waitcnt vmcnt(11)
	v_mul_f32_e32 v5, 0x43800000, v6
	s_waitcnt vmcnt(10)
	v_mul_f32_e32 v6, 0x43800000, v10
	v_cvt_pk_fp8_f32 v4, v14, v15 op_sel:[0,0,1]
	v_med3_f32 v15, v5, s54, v192
	v_med3_f32 v6, v6, s54, v192
	v_mov_b32_e32 v5, v163
	v_cvt_pk_fp8_f32 v5, v15, v6
	s_waitcnt vmcnt(9)
	v_mul_f32_e32 v10, 0x43800000, v34
	s_waitcnt vmcnt(8)
	v_mul_f32_e32 v14, 0x43800000, v42
	v_med3_f32 v10, v10, s54, v192
	v_med3_f32 v14, v14, s54, v192
	v_cvt_pk_fp8_f32 v5, v10, v14 op_sel:[0,0,1]
	ds_write_b128 v1, v[2:5] offset:34816
	v_mul_f32_e32 v2, 0x43800000, v95
	v_mul_f32_e32 v3, 0x43800000, v103
	v_med3_f32 v6, v2, s54, v192
	v_med3_f32 v3, v3, s54, v192
	v_mov_b32_e32 v2, v163
	v_cvt_pk_fp8_f32 v2, v6, v3
	v_mul_f32_e32 v4, 0x43800000, v123
	v_mul_f32_e32 v5, 0x43800000, v127
	v_med3_f32 v4, v4, s54, v192
	v_med3_f32 v5, v5, s54, v192
	v_cvt_pk_fp8_f32 v2, v4, v5 op_sel:[0,0,1]
	v_mul_f32_e32 v3, 0x43800000, v59
	v_mul_f32_e32 v4, 0x43800000, v71
	v_med3_f32 v10, v3, s54, v192
	v_med3_f32 v4, v4, s54, v192
	v_mov_b32_e32 v3, v163
	v_cvt_pk_fp8_f32 v3, v10, v4
	v_mul_f32_e32 v5, 0x43800000, v99
	v_mul_f32_e32 v6, 0x43800000, v107
	v_med3_f32 v5, v5, s54, v192
	v_med3_f32 v6, v6, s54, v192
	v_cvt_pk_fp8_f32 v3, v5, v6 op_sel:[0,0,1]
	v_mul_f32_e32 v4, 0x43800000, v27
	v_mul_f32_e32 v5, 0x43800000, v39
	v_med3_f32 v14, v4, s54, v192
	v_med3_f32 v5, v5, s54, v192
	v_mov_b32_e32 v4, v163
	v_cvt_pk_fp8_f32 v4, v14, v5
	v_mul_f32_e32 v6, 0x43800000, v67
	v_mul_f32_e32 v10, 0x43800000, v75
	v_med3_f32 v6, v6, s54, v192
	v_med3_f32 v10, v10, s54, v192
	v_cvt_pk_fp8_f32 v4, v6, v10 op_sel:[0,0,1]
	v_mul_f32_e32 v5, 0x43800000, v7
	v_mul_f32_e32 v6, 0x43800000, v11
	v_med3_f32 v11, v5, s54, v192
	v_med3_f32 v6, v6, s54, v192
	v_mov_b32_e32 v5, v163
	v_cvt_pk_fp8_f32 v5, v11, v6
	v_mul_f32_e32 v7, 0x43800000, v35
	v_mul_f32_e32 v10, 0x43800000, v43
	v_med3_f32 v7, v7, s54, v192
	v_med3_f32 v10, v10, s54, v192
	v_cvt_pk_fp8_f32 v5, v7, v10 op_sel:[0,0,1]
	ds_write_b128 v1, v[2:5] offset:35088
	v_mul_f32_e32 v2, 0x43800000, v96
	v_mul_f32_e32 v3, 0x43800000, v104
	v_med3_f32 v6, v2, s54, v192
	v_med3_f32 v3, v3, s54, v192
	v_mov_b32_e32 v2, v163
	v_cvt_pk_fp8_f32 v2, v6, v3
	v_mul_f32_e32 v4, 0x43800000, v124
	v_mul_f32_e32 v5, 0x43800000, v128
	v_med3_f32 v4, v4, s54, v192
	v_med3_f32 v5, v5, s54, v192
	v_cvt_pk_fp8_f32 v2, v4, v5 op_sel:[0,0,1]
	v_mul_f32_e32 v3, 0x43800000, v60
	v_mul_f32_e32 v4, 0x43800000, v72
	v_med3_f32 v7, v3, s54, v192
	v_med3_f32 v4, v4, s54, v192
	v_mov_b32_e32 v3, v163
	v_cvt_pk_fp8_f32 v3, v7, v4
	v_mul_f32_e32 v5, 0x43800000, v100
	v_mul_f32_e32 v6, 0x43800000, v108
	v_med3_f32 v5, v5, s54, v192
	v_med3_f32 v6, v6, s54, v192
	v_cvt_pk_fp8_f32 v3, v5, v6 op_sel:[0,0,1]
	v_mul_f32_e32 v4, 0x43800000, v28
	v_mul_f32_e32 v5, 0x43800000, v40
	v_med3_f32 v10, v4, s54, v192
	v_med3_f32 v5, v5, s54, v192
	v_mov_b32_e32 v4, v163
	v_cvt_pk_fp8_f32 v4, v10, v5
	v_mul_f32_e32 v6, 0x43800000, v68
	v_mul_f32_e32 v7, 0x43800000, v76
	v_med3_f32 v6, v6, s54, v192
	v_med3_f32 v7, v7, s54, v192
	v_cvt_pk_fp8_f32 v4, v6, v7 op_sel:[0,0,1]
	v_mul_f32_e32 v5, 0x43800000, v8
	v_mul_f32_e32 v6, 0x43800000, v12
	v_med3_f32 v10, v5, s54, v192
	v_med3_f32 v6, v6, s54, v192
	v_mov_b32_e32 v5, v163
	v_cvt_pk_fp8_f32 v5, v10, v6
	v_mul_f32_e32 v7, 0x43800000, v36
	v_mul_f32_e32 v8, 0x43800000, v44
	v_med3_f32 v7, v7, s54, v192
	v_med3_f32 v8, v8, s54, v192
	v_cvt_pk_fp8_f32 v5, v7, v8 op_sel:[0,0,1]
	ds_write_b128 v1, v[2:5] offset:35360
	v_mul_f32_e32 v2, 0x43800000, v97
	v_mul_f32_e32 v3, 0x43800000, v105
	v_med3_f32 v6, v2, s54, v192
	v_med3_f32 v3, v3, s54, v192
	v_mov_b32_e32 v2, v163
	v_cvt_pk_fp8_f32 v2, v6, v3
	v_mul_f32_e32 v4, 0x43800000, v125
	v_mul_f32_e32 v5, 0x43800000, v129
	v_med3_f32 v4, v4, s54, v192
	v_med3_f32 v5, v5, s54, v192
	v_cvt_pk_fp8_f32 v2, v4, v5 op_sel:[0,0,1]
	v_mul_f32_e32 v3, 0x43800000, v61
	v_mul_f32_e32 v4, 0x43800000, v73
	v_med3_f32 v7, v3, s54, v192
	v_med3_f32 v4, v4, s54, v192
	v_mov_b32_e32 v3, v163
	v_cvt_pk_fp8_f32 v3, v7, v4
	v_mul_f32_e32 v5, 0x43800000, v101
	v_mul_f32_e32 v6, 0x43800000, v109
	v_med3_f32 v5, v5, s54, v192
	v_med3_f32 v6, v6, s54, v192
	v_cvt_pk_fp8_f32 v3, v5, v6 op_sel:[0,0,1]
	v_mul_f32_e32 v4, 0x43800000, v29
	v_mul_f32_e32 v5, 0x43800000, v41
	v_med3_f32 v8, v4, s54, v192
	v_med3_f32 v5, v5, s54, v192
	v_mov_b32_e32 v4, v163
	v_cvt_pk_fp8_f32 v4, v8, v5
	v_mul_f32_e32 v6, 0x43800000, v69
	v_mul_f32_e32 v7, 0x43800000, v77
	v_med3_f32 v6, v6, s54, v192
	v_med3_f32 v7, v7, s54, v192
	v_cvt_pk_fp8_f32 v4, v6, v7 op_sel:[0,0,1]
	v_mul_f32_e32 v5, 0x43800000, v9
	v_mul_f32_e32 v6, 0x43800000, v13
	v_med3_f32 v9, v5, s54, v192
	v_med3_f32 v6, v6, s54, v192
	v_mov_b32_e32 v5, v163
	v_cvt_pk_fp8_f32 v5, v9, v6
	v_mul_f32_e32 v7, 0x43800000, v37
	v_mul_f32_e32 v8, 0x43800000, v45
	v_med3_f32 v7, v7, s54, v192
	v_med3_f32 v8, v8, s54, v192
	v_cvt_pk_fp8_f32 v5, v7, v8 op_sel:[0,0,1]
	ds_write_b128 v1, v[2:5] offset:35632
	s_waitcnt lgkmcnt(0)
	s_barrier
	ds_read_b128 v[2:5], v146 offset:34816
	s_waitcnt lgkmcnt(0)
	global_store_dwordx4 v[148:149], v[2:5], off offset:1792 nt
	ds_read_b128 v[2:5], v150 offset:34816
	s_waitcnt lgkmcnt(0)
	global_store_dwordx4 v[152:153], v[2:5], off offset:1792 nt
	ds_read_b128 v[2:5], v154 offset:34816
	s_waitcnt lgkmcnt(0)
	global_store_dwordx4 v[156:157], v[2:5], off offset:1792 nt
	ds_read_b128 v[2:5], v158 offset:34816
	s_waitcnt lgkmcnt(0)
	global_store_dwordx4 v[160:161], v[2:5], off offset:1792 nt
	s_mov_b64 s[10:11], 0
	s_mov_b32 s2, s0
	s_barrier

.LBB0_834:
	s_cmp_eq_u32 s7, 4
	s_mov_b64 s[12:13], -1
	s_cbranch_scc0 .LBB0_840
	s_cmpk_gt_i32 s0, 0x27f
	s_cbranch_scc0 .LBB0_837
	s_add_i32 s2, s1, 0xffffff80
	v_readlane_b32 s16, v254, 30
	s_cmp_lt_u32 s2, 64
	s_mov_b32 s10, 0x3000000
	v_readlane_b32 s22, v254, 36
	v_readlane_b32 s23, v254, 37
	v_readlane_b32 s24, v254, 38
	v_readlane_b32 s25, v254, 39
	s_cselect_b32 s10, s10, 0x3400000
	s_cselect_b32 s11, s23, s25
	s_cselect_b32 s12, s22, s24
	s_lshl_b32 s13, s2, 8
	s_and_b32 s15, s13, 0x300
	s_lshl_b32 s13, s15, 13
	s_add_u32 s12, s12, s13
	s_addc_u32 s11, s11, 0
	s_lshl_b32 s2, s2, 5
	s_and_b32 s2, s2, 0x780
	s_lshl_b32 s13, s2, 2
	v_readlane_b32 s17, v254, 31
	s_add_u32 s12, s12, s13
	s_addc_u32 s13, s11, 0
	v_readlane_b32 s16, v254, 57
	v_readlane_b32 s17, v254, 58
	s_add_u32 s10, s16, s10
	s_addc_u32 s11, s17, 0
	s_lshl_b32 s2, s2, 10
	s_add_u32 s2, s10, s2
	v_mov_b32_e32 v1, v0
	s_addc_u32 s11, s11, 0
	s_add_u32 s10, s2, s15
	v_readfirstlane_b32 s14, v1
	s_addc_u32 s11, s11, 0
	s_ashr_i32 s2, s14, 1
	v_lshrrev_b32_e32 v2, 1, v1
	s_andn2_b32 s2, s2, 31
	v_and_b32_e32 v70, 16, v2
	v_or_b32_e32 v2, s2, v70
	v_ashrrev_i32_e32 v3, 31, v2
	v_lshlrev_b32_e32 v4, 2, v1
	v_lshlrev_b64 v[2:3], 13, v[2:3]
	v_and_b32_e32 v71, 0x7c, v4
	v_lshl_add_u64 v[2:3], s[12:13], 0, v[2:3]
	v_lshlrev_b32_e32 v162, 2, v71
	s_waitcnt vmcnt(20)
	v_lshl_add_u64 v[50:51], v[2:3], 0, v[162:163]
	v_add_co_u32_e32 v2, vcc, s44, v50
	s_movk_i32 s12, 0x4000
	s_nop 0
	v_addc_co_u32_e32 v3, vcc, 0, v51, vcc
	s_barrier
	global_load_dwordx4 v[14:17], v[50:51], off sc0 nt
	global_load_dwordx4 v[18:21], v[2:3], off sc0 nt
	v_add_co_u32_e32 v2, vcc, s12, v50
	s_movk_i32 s12, 0x6000
	s_nop 0
	v_addc_co_u32_e32 v3, vcc, 0, v51, vcc
	global_load_dwordx4 v[34:37], v[2:3], off sc0 nt
	v_add_co_u32_e32 v2, vcc, s12, v50
	s_mov_b32 s12, 0x8000
	s_nop 0
	v_addc_co_u32_e32 v3, vcc, 0, v51, vcc
	global_load_dwordx4 v[54:57], v[2:3], off sc0 nt
	v_add_co_u32_e32 v2, vcc, s12, v50
	s_mov_b32 s12, 0xa000
	s_nop 0
	v_addc_co_u32_e32 v3, vcc, 0, v51, vcc
	v_add_co_u32_e32 v6, vcc, s12, v50
	s_mov_b32 s12, 0xc000
	s_nop 0
	v_addc_co_u32_e32 v7, vcc, 0, v51, vcc
	global_load_dwordx4 v[2:5], v[2:3], off sc0 nt
	v_mov_b32_e32 v66, v163
	global_load_dwordx4 v[22:25], v[6:7], off sc0 nt
	v_add_co_u32_e32 v6, vcc, s12, v50
	s_mov_b32 s12, 0xe000
	s_nop 0
	v_addc_co_u32_e32 v7, vcc, 0, v51, vcc
	global_load_dwordx4 v[38:41], v[6:7], off sc0 nt
	v_add_co_u32_e32 v6, vcc, s12, v50
	s_mov_b32 s12, 0x10000
	s_nop 0
	v_addc_co_u32_e32 v7, vcc, 0, v51, vcc
	global_load_dwordx4 v[58:61], v[6:7], off sc0 nt
	v_add_co_u32_e32 v6, vcc, s12, v50
	s_mov_b32 s12, 0x12000
	s_nop 0
	v_addc_co_u32_e32 v7, vcc, 0, v51, vcc
	v_add_co_u32_e32 v10, vcc, s12, v50
	s_mov_b32 s12, 0x14000
	s_nop 0
	v_addc_co_u32_e32 v11, vcc, 0, v51, vcc
	global_load_dwordx4 v[6:9], v[6:7], off sc0 nt
	v_mov_b32_e32 v67, v163
	global_load_dwordx4 v[26:29], v[10:11], off sc0 nt
	v_add_co_u32_e32 v10, vcc, s12, v50
	s_mov_b32 s12, 0x16000
	s_nop 0
	v_addc_co_u32_e32 v11, vcc, 0, v51, vcc
	global_load_dwordx4 v[42:45], v[10:11], off sc0 nt
	v_add_co_u32_e32 v10, vcc, s12, v50
	s_mov_b32 s12, 0x18000
	s_nop 0
	v_addc_co_u32_e32 v11, vcc, 0, v51, vcc
	global_load_dwordx4 v[62:65], v[10:11], off sc0 nt
	v_add_co_u32_e32 v10, vcc, s12, v50
	s_mov_b32 s12, 0x1a000
	s_nop 0
	v_addc_co_u32_e32 v11, vcc, 0, v51, vcc
	v_add_co_u32_e32 v30, vcc, s12, v50
	s_mov_b32 s12, 0x1c000
	s_nop 0
	v_addc_co_u32_e32 v31, vcc, 0, v51, vcc
	global_load_dwordx4 v[10:13], v[10:11], off sc0 nt
	s_waitcnt vmcnt(32)
	v_add_co_u32_e32 v46, vcc, s12, v50
	global_load_dwordx4 v[30:33], v[30:31], off sc0 nt
	s_nop 0
	v_addc_co_u32_e32 v47, vcc, 0, v51, vcc
	s_mov_b32 s12, 0x1e000
	v_add_co_u32_e32 v50, vcc, s12, v50
	global_load_dwordx4 v[46:49], v[46:47], off sc0 nt
	s_nop 0
	v_addc_co_u32_e32 v51, vcc, 0, v51, vcc
	global_load_dwordx4 v[50:53], v[50:51], off sc0 nt
	s_waitcnt vmcnt(15)
	v_mul_f32_e32 v14, 0x43800000, v14
	s_waitcnt vmcnt(14)
	v_mul_f32_e32 v18, 0x43800000, v18
	v_med3_f32 v14, v14, s54, v192
	v_med3_f32 v18, v18, s54, v192
	v_cvt_pk_fp8_f32 v66, v14, v18
	v_mov_b32_e32 v68, v163
	v_mov_b32_e32 v69, v163
	s_waitcnt vmcnt(13)
	v_mul_f32_e32 v34, 0x43800000, v34
	s_waitcnt vmcnt(12)
	v_mul_f32_e32 v54, 0x43800000, v54
	v_med3_f32 v34, v34, s54, v192
	v_med3_f32 v54, v54, s54, v192
	v_cvt_pk_fp8_f32 v66, v34, v54 op_sel:[0,0,1]
	s_add_i32 s2, s2, 0
	v_readlane_b32 s18, v254, 32
	v_readlane_b32 s19, v254, 33
	v_readlane_b32 s20, v254, 34
	v_readlane_b32 s21, v254, 35
	s_waitcnt vmcnt(11)
	v_mul_f32_e32 v2, 0x43800000, v2
	v_med3_f32 v2, v2, s54, v192
	s_waitcnt vmcnt(10)
	v_mul_f32_e32 v14, 0x43800000, v22
	v_med3_f32 v14, v14, s54, v192
	v_cvt_pk_fp8_f32 v67, v2, v14
	v_readlane_b32 s26, v254, 40
	v_readlane_b32 s27, v254, 41
	v_readlane_b32 s28, v254, 42
	s_waitcnt vmcnt(9)
	v_mul_f32_e32 v18, 0x43800000, v38
	v_med3_f32 v18, v18, s54, v192
	v_readlane_b32 s29, v254, 43
	v_readlane_b32 s30, v254, 44
	v_readlane_b32 s31, v254, 45
	s_waitcnt vmcnt(8)
	v_mul_f32_e32 v22, 0x43800000, v58
	v_med3_f32 v22, v22, s54, v192
	v_cvt_pk_fp8_f32 v67, v18, v22 op_sel:[0,0,1]
	s_waitcnt vmcnt(7)
	v_mul_f32_e32 v2, 0x43800000, v6
	v_med3_f32 v2, v2, s54, v192
	s_waitcnt vmcnt(6)
	v_mul_f32_e32 v6, 0x43800000, v26
	v_med3_f32 v6, v6, s54, v192
	v_cvt_pk_fp8_f32 v68, v2, v6
	s_waitcnt vmcnt(5)
	v_mul_f32_e32 v14, 0x43800000, v42
	v_med3_f32 v14, v14, s54, v192
	s_waitcnt vmcnt(4)
	v_mul_f32_e32 v18, 0x43800000, v62
	v_med3_f32 v18, v18, s54, v192
	v_cvt_pk_fp8_f32 v68, v14, v18 op_sel:[0,0,1]
	s_waitcnt vmcnt(3)
	v_mul_f32_e32 v2, 0x43800000, v10
	v_med3_f32 v2, v2, s54, v192
	s_waitcnt vmcnt(2)
	v_mul_f32_e32 v6, 0x43800000, v30
	v_med3_f32 v6, v6, s54, v192
	v_cvt_pk_fp8_f32 v69, v2, v6
	v_mul_u32_u24_e32 v2, 0x110, v71
	v_add3_u32 v6, s2, v70, v2
	v_mul_f32_e32 v2, 0x43800000, v15
	s_waitcnt vmcnt(1)
	v_mul_f32_e32 v10, 0x43800000, v46
	v_med3_f32 v10, v10, s54, v192
	v_med3_f32 v2, v2, s54, v192
	s_waitcnt vmcnt(0)
	v_mul_f32_e32 v14, 0x43800000, v50
	v_med3_f32 v14, v14, s54, v192
	v_cvt_pk_fp8_f32 v69, v10, v14 op_sel:[0,0,1]
	v_mul_f32_e32 v10, 0x43800000, v19
	v_med3_f32 v10, v10, s54, v192
	v_mul_f32_e32 v14, 0x43800000, v35
	ds_write_b128 v6, v[66:69]
	v_mov_b32_e32 v66, v163
	v_cvt_pk_fp8_f32 v66, v2, v10
	v_mul_f32_e32 v2, 0x43800000, v3
	v_mul_f32_e32 v3, 0x43800000, v23
	v_med3_f32 v2, v2, s54, v192
	v_med3_f32 v3, v3, s54, v192
	v_mov_b32_e32 v67, v163
	v_mul_f32_e32 v15, 0x43800000, v55
	v_cvt_pk_fp8_f32 v67, v2, v3
	v_mul_f32_e32 v2, 0x43800000, v7
	v_mul_f32_e32 v3, 0x43800000, v27
	v_med3_f32 v14, v14, s54, v192
	v_med3_f32 v15, v15, s54, v192
	v_med3_f32 v2, v2, s54, v192
	v_med3_f32 v3, v3, s54, v192
	v_mov_b32_e32 v68, v163
	v_cvt_pk_fp8_f32 v66, v14, v15 op_sel:[0,0,1]
	v_mul_f32_e32 v10, 0x43800000, v39
	v_mul_f32_e32 v14, 0x43800000, v59
	v_cvt_pk_fp8_f32 v68, v2, v3
	v_mul_f32_e32 v2, 0x43800000, v11
	v_mul_f32_e32 v3, 0x43800000, v31
	v_med3_f32 v10, v10, s54, v192
	v_med3_f32 v14, v14, s54, v192
	v_med3_f32 v2, v2, s54, v192
	v_med3_f32 v3, v3, s54, v192
	v_mov_b32_e32 v69, v163
	v_cvt_pk_fp8_f32 v67, v10, v14 op_sel:[0,0,1]
	v_mul_f32_e32 v7, 0x43800000, v43
	v_mul_f32_e32 v10, 0x43800000, v63
	v_cvt_pk_fp8_f32 v69, v2, v3
	v_med3_f32 v7, v7, s54, v192
	v_med3_f32 v10, v10, s54, v192
	v_cvt_pk_fp8_f32 v68, v7, v10 op_sel:[0,0,1]
	v_mul_f32_e32 v7, 0x43800000, v47
	v_mul_f32_e32 v10, 0x43800000, v51
	v_med3_f32 v7, v7, s54, v192
	v_med3_f32 v10, v10, s54, v192
	v_cvt_pk_fp8_f32 v69, v7, v10 op_sel:[0,0,1]
	v_mul_f32_e32 v2, 0x43800000, v16
	v_mul_f32_e32 v3, 0x43800000, v20
	v_med3_f32 v2, v2, s54, v192
	ds_write_b128 v6, v[66:69] offset:272
	v_med3_f32 v3, v3, s54, v192
	v_mov_b32_e32 v66, v163
	v_cvt_pk_fp8_f32 v66, v2, v3
	v_mul_f32_e32 v2, 0x43800000, v4
	v_mul_f32_e32 v3, 0x43800000, v24
	v_med3_f32 v2, v2, s54, v192
	v_med3_f32 v3, v3, s54, v192
	v_mov_b32_e32 v67, v163
	v_mul_f32_e32 v7, 0x43800000, v36
	v_mul_f32_e32 v10, 0x43800000, v56
	v_cvt_pk_fp8_f32 v67, v2, v3
	v_mul_f32_e32 v2, 0x43800000, v8
	v_mul_f32_e32 v3, 0x43800000, v28
	v_med3_f32 v7, v7, s54, v192
	v_med3_f32 v10, v10, s54, v192
	v_med3_f32 v2, v2, s54, v192
	v_med3_f32 v3, v3, s54, v192
	v_mov_b32_e32 v68, v163
	v_cvt_pk_fp8_f32 v66, v7, v10 op_sel:[0,0,1]
	v_mul_f32_e32 v4, 0x43800000, v40
	v_mul_f32_e32 v7, 0x43800000, v60
	v_cvt_pk_fp8_f32 v68, v2, v3
	v_mul_f32_e32 v2, 0x43800000, v12
	v_mul_f32_e32 v3, 0x43800000, v32
	v_med3_f32 v4, v4, s54, v192
	v_med3_f32 v7, v7, s54, v192
	v_med3_f32 v2, v2, s54, v192
	v_med3_f32 v3, v3, s54, v192
	v_mov_b32_e32 v69, v163
	v_cvt_pk_fp8_f32 v67, v4, v7 op_sel:[0,0,1]
	v_mul_f32_e32 v4, 0x43800000, v44
	v_mul_f32_e32 v7, 0x43800000, v64
	v_cvt_pk_fp8_f32 v69, v2, v3
	v_mul_f32_e32 v2, 0x43800000, v17
	v_mul_f32_e32 v3, 0x43800000, v21
	v_med3_f32 v4, v4, s54, v192
	v_med3_f32 v7, v7, s54, v192
	v_med3_f32 v8, v2, s54, v192
	v_med3_f32 v3, v3, s54, v192
	v_mov_b32_e32 v2, v163
	v_cvt_pk_fp8_f32 v68, v4, v7 op_sel:[0,0,1]
	v_mul_f32_e32 v4, 0x43800000, v48
	v_mul_f32_e32 v7, 0x43800000, v52
	v_cvt_pk_fp8_f32 v2, v8, v3
	v_med3_f32 v4, v4, s54, v192
	v_med3_f32 v7, v7, s54, v192
	v_cvt_pk_fp8_f32 v69, v4, v7 op_sel:[0,0,1]
	v_mul_f32_e32 v4, 0x43800000, v37
	v_mul_f32_e32 v7, 0x43800000, v57
	v_med3_f32 v4, v4, s54, v192
	v_med3_f32 v7, v7, s54, v192
	v_cvt_pk_fp8_f32 v2, v4, v7 op_sel:[0,0,1]
	v_mul_f32_e32 v3, 0x43800000, v5
	v_mul_f32_e32 v4, 0x43800000, v25
	v_med3_f32 v8, v3, s54, v192
	v_med3_f32 v4, v4, s54, v192
	v_mov_b32_e32 v3, v163
	v_cvt_pk_fp8_f32 v3, v8, v4
	v_mul_f32_e32 v5, 0x43800000, v41
	v_mul_f32_e32 v7, 0x43800000, v61
	v_med3_f32 v5, v5, s54, v192
	v_med3_f32 v7, v7, s54, v192
	v_cvt_pk_fp8_f32 v3, v5, v7 op_sel:[0,0,1]
	v_mul_f32_e32 v4, 0x43800000, v9
	v_mul_f32_e32 v5, 0x43800000, v29
	v_med3_f32 v9, v4, s54, v192
	v_med3_f32 v5, v5, s54, v192
	v_mov_b32_e32 v4, v163
	v_cvt_pk_fp8_f32 v4, v9, v5
	v_mul_f32_e32 v7, 0x43800000, v45
	v_mul_f32_e32 v8, 0x43800000, v65
	v_med3_f32 v7, v7, s54, v192
	v_med3_f32 v8, v8, s54, v192
	v_cvt_pk_fp8_f32 v4, v7, v8 op_sel:[0,0,1]
	v_mul_f32_e32 v5, 0x43800000, v13
	v_mul_f32_e32 v7, 0x43800000, v33
	v_med3_f32 v10, v5, s54, v192
	v_med3_f32 v7, v7, s54, v192
	v_mov_b32_e32 v5, v163
	v_cvt_pk_fp8_f32 v5, v10, v7
	v_mul_f32_e32 v8, 0x43800000, v49
	v_mul_f32_e32 v9, 0x43800000, v53
	v_med3_f32 v8, v8, s54, v192
	v_med3_f32 v9, v9, s54, v192
	v_cvt_pk_fp8_f32 v5, v8, v9 op_sel:[0,0,1]
	v_ashrrev_i32_e32 v8, 4, v1
	ds_write_b128 v6, v[66:69] offset:544
	v_ashrrev_i32_e32 v9, 31, v8
	ds_write_b128 v6, v[2:5] offset:816
	v_lshlrev_b32_e32 v2, 4, v1
	v_and_b32_e32 v162, 0xf0, v2
	v_mul_lo_u32 v2, v8, s55
	v_add3_u32 v2, 0, v2, v162
	s_waitcnt lgkmcnt(0)
	s_barrier
	ds_read_b128 v[2:5], v2
	v_lshl_add_u64 v[6:7], s[10:11], 0, v[162:163]
	v_lshlrev_b64 v[8:9], 10, v[8:9]
	v_lshl_add_u64 v[8:9], v[6:7], 0, v[8:9]
	s_mov_b64 s[10:11], 0
	s_waitcnt lgkmcnt(0)
	global_store_dwordx4 v[8:9], v[2:5], off
	s_nop 1
	v_add_u32_e32 v2, 0x200, v1
	v_ashrrev_i32_e32 v8, 4, v2
	v_mul_lo_u32 v2, v8, s55
	v_add3_u32 v2, 0, v2, v162
	ds_read_b128 v[2:5], v2
	v_ashrrev_i32_e32 v9, 31, v8
	v_lshlrev_b64 v[8:9], 10, v[8:9]
	v_lshl_add_u64 v[8:9], v[6:7], 0, v[8:9]
	s_waitcnt lgkmcnt(0)
	global_store_dwordx4 v[8:9], v[2:5], off
	s_nop 1
	v_add_u32_e32 v2, 0x400, v1
	v_ashrrev_i32_e32 v8, 4, v2
	v_mul_lo_u32 v2, v8, s55
	v_add3_u32 v2, 0, v2, v162
	ds_read_b128 v[2:5], v2
	v_ashrrev_i32_e32 v9, 31, v8
	v_lshlrev_b64 v[8:9], 10, v[8:9]
	v_lshl_add_u64 v[8:9], v[6:7], 0, v[8:9]
	v_add_u32_e32 v1, 0x600, v1
	s_waitcnt lgkmcnt(0)
	global_store_dwordx4 v[8:9], v[2:5], off
	v_ashrrev_i32_e32 v8, 4, v1
	v_mul_lo_u32 v1, v8, s55
	v_add3_u32 v1, 0, v1, v162
	ds_read_b128 v[2:5], v1
	v_ashrrev_i32_e32 v9, 31, v8
	v_lshlrev_b64 v[8:9], 10, v[8:9]
	v_lshl_add_u64 v[6:7], v[6:7], 0, v[8:9]
	s_waitcnt lgkmcnt(0)
	global_store_dwordx4 v[6:7], v[2:5], off
	s_barrier
.LBB0_837:
	s_andn2_b64 vcc, exec, s[10:11]
	s_cbranch_vccnz .LBB0_839
	s_lshl_b32 s10, s1, 8
	s_and_b32 s14, s10, 0x700
	v_readlane_b32 s16, v254, 30
	s_lshl_b32 s10, s14, 13
	v_readlane_b32 s26, v254, 40
	v_readlane_b32 s27, v254, 41
	s_add_u32 s15, s26, s10
	s_addc_u32 s16, s27, 0
	s_lshl_b32 s10, s1, 4
	s_and_b32 s10, s10, 0xffffff80
	s_ashr_i32 s11, s10, 31
	s_lshl_b64 s[12:13], s[10:11], 2
	s_add_u32 s12, s15, s12
	s_addc_u32 s13, s16, s13
	s_lshl_b64 s[10:11], s[10:11], 11
	v_readlane_b32 s15, v255, 13
	s_add_u32 s10, s15, s10
	v_readlane_b32 s15, v255, 14
	v_mov_b32_e32 v1, v0
	s_addc_u32 s11, s15, s11
	s_add_u32 s10, s10, s14
	v_readfirstlane_b32 s2, v1
	s_addc_u32 s11, s11, 0
	s_ashr_i32 s2, s2, 1
	v_lshrrev_b32_e32 v2, 1, v1
	s_andn2_b32 s2, s2, 31
	v_and_b32_e32 v70, 16, v2
	v_or_b32_e32 v2, s2, v70
	v_ashrrev_i32_e32 v3, 31, v2
	v_lshlrev_b32_e32 v4, 2, v1
	v_lshlrev_b64 v[2:3], 13, v[2:3]
	v_and_b32_e32 v71, 0x7c, v4
	v_lshl_add_u64 v[2:3], s[12:13], 0, v[2:3]
	v_lshlrev_b32_e32 v162, 2, v71
	s_waitcnt vmcnt(20)
	v_lshl_add_u64 v[50:51], v[2:3], 0, v[162:163]
	v_add_co_u32_e32 v2, vcc, s44, v50
	s_movk_i32 s12, 0x4000
	s_nop 0
	v_addc_co_u32_e32 v3, vcc, 0, v51, vcc
	s_barrier
	global_load_dwordx4 v[14:17], v[50:51], off sc0 nt
	global_load_dwordx4 v[18:21], v[2:3], off sc0 nt
	v_add_co_u32_e32 v2, vcc, s12, v50
	s_movk_i32 s12, 0x6000
	s_nop 0
	v_addc_co_u32_e32 v3, vcc, 0, v51, vcc
	global_load_dwordx4 v[34:37], v[2:3], off sc0 nt
	v_add_co_u32_e32 v2, vcc, s12, v50
	s_mov_b32 s12, 0x8000
	s_nop 0
	v_addc_co_u32_e32 v3, vcc, 0, v51, vcc
	global_load_dwordx4 v[54:57], v[2:3], off sc0 nt
	v_add_co_u32_e32 v2, vcc, s12, v50
	s_mov_b32 s12, 0xa000
	s_nop 0
	v_addc_co_u32_e32 v3, vcc, 0, v51, vcc
	v_add_co_u32_e32 v6, vcc, s12, v50
	s_mov_b32 s12, 0xc000
	s_nop 0
	v_addc_co_u32_e32 v7, vcc, 0, v51, vcc
	global_load_dwordx4 v[2:5], v[2:3], off sc0 nt
	v_mov_b32_e32 v66, v163
	global_load_dwordx4 v[22:25], v[6:7], off sc0 nt
	v_add_co_u32_e32 v6, vcc, s12, v50
	s_mov_b32 s12, 0xe000
	s_nop 0
	v_addc_co_u32_e32 v7, vcc, 0, v51, vcc
	global_load_dwordx4 v[38:41], v[6:7], off sc0 nt
	v_add_co_u32_e32 v6, vcc, s12, v50
	s_mov_b32 s12, 0x10000
	s_nop 0
	v_addc_co_u32_e32 v7, vcc, 0, v51, vcc
	global_load_dwordx4 v[58:61], v[6:7], off sc0 nt
	v_add_co_u32_e32 v6, vcc, s12, v50
	s_mov_b32 s12, 0x12000
	s_nop 0
	v_addc_co_u32_e32 v7, vcc, 0, v51, vcc
	v_add_co_u32_e32 v10, vcc, s12, v50
	s_mov_b32 s12, 0x14000
	s_nop 0
	v_addc_co_u32_e32 v11, vcc, 0, v51, vcc
	global_load_dwordx4 v[6:9], v[6:7], off sc0 nt
	v_mov_b32_e32 v67, v163
	global_load_dwordx4 v[26:29], v[10:11], off sc0 nt
	v_add_co_u32_e32 v10, vcc, s12, v50
	s_mov_b32 s12, 0x16000
	s_nop 0
	v_addc_co_u32_e32 v11, vcc, 0, v51, vcc
	global_load_dwordx4 v[42:45], v[10:11], off sc0 nt
	v_add_co_u32_e32 v10, vcc, s12, v50
	s_mov_b32 s12, 0x18000
	s_nop 0
	v_addc_co_u32_e32 v11, vcc, 0, v51, vcc
	global_load_dwordx4 v[62:65], v[10:11], off sc0 nt
	v_add_co_u32_e32 v10, vcc, s12, v50
	s_mov_b32 s12, 0x1a000
	s_nop 0
	v_addc_co_u32_e32 v11, vcc, 0, v51, vcc
	v_add_co_u32_e32 v30, vcc, s12, v50
	s_mov_b32 s12, 0x1c000
	s_nop 0
	v_addc_co_u32_e32 v31, vcc, 0, v51, vcc
	global_load_dwordx4 v[10:13], v[10:11], off sc0 nt
	s_waitcnt vmcnt(32)
	v_add_co_u32_e32 v46, vcc, s12, v50
	global_load_dwordx4 v[30:33], v[30:31], off sc0 nt
	s_nop 0
	v_addc_co_u32_e32 v47, vcc, 0, v51, vcc
	s_mov_b32 s12, 0x1e000
	v_add_co_u32_e32 v50, vcc, s12, v50
	global_load_dwordx4 v[46:49], v[46:47], off sc0 nt
	s_nop 0
	v_addc_co_u32_e32 v51, vcc, 0, v51, vcc
	global_load_dwordx4 v[50:53], v[50:51], off sc0 nt
	s_waitcnt vmcnt(15)
	v_mul_f32_e32 v14, 0x43800000, v14
	s_waitcnt vmcnt(14)
	v_mul_f32_e32 v18, 0x43800000, v18
	v_med3_f32 v14, v14, s54, v192
	v_med3_f32 v18, v18, s54, v192
	v_cvt_pk_fp8_f32 v66, v14, v18
	v_mov_b32_e32 v68, v163
	v_mov_b32_e32 v69, v163
	s_waitcnt vmcnt(13)
	v_mul_f32_e32 v34, 0x43800000, v34
	s_waitcnt vmcnt(12)
	v_mul_f32_e32 v54, 0x43800000, v54
	v_med3_f32 v34, v34, s54, v192
	v_med3_f32 v54, v54, s54, v192
	v_cvt_pk_fp8_f32 v66, v34, v54 op_sel:[0,0,1]
	s_add_i32 s2, s2, 0
	v_readlane_b32 s17, v254, 31
	v_readlane_b32 s18, v254, 32
	v_readlane_b32 s19, v254, 33
	v_readlane_b32 s20, v254, 34
	s_waitcnt vmcnt(11)
	v_mul_f32_e32 v2, 0x43800000, v2
	v_med3_f32 v2, v2, s54, v192
	s_waitcnt vmcnt(10)
	v_mul_f32_e32 v14, 0x43800000, v22
	v_med3_f32 v14, v14, s54, v192
	v_cvt_pk_fp8_f32 v67, v2, v14
	v_readlane_b32 s21, v254, 35
	v_readlane_b32 s22, v254, 36
	v_readlane_b32 s23, v254, 37
	s_waitcnt vmcnt(9)
	v_mul_f32_e32 v18, 0x43800000, v38
	v_med3_f32 v18, v18, s54, v192
	v_readlane_b32 s24, v254, 38
	v_readlane_b32 s25, v254, 39
	v_readlane_b32 s28, v254, 42
	v_readlane_b32 s29, v254, 43
	s_waitcnt vmcnt(8)
	v_mul_f32_e32 v22, 0x43800000, v58
	v_med3_f32 v22, v22, s54, v192
	v_cvt_pk_fp8_f32 v67, v18, v22 op_sel:[0,0,1]
	v_readlane_b32 s30, v254, 44
	v_readlane_b32 s31, v254, 45
	s_waitcnt vmcnt(7)
	v_mul_f32_e32 v2, 0x43800000, v6
	v_med3_f32 v2, v2, s54, v192
	s_waitcnt vmcnt(6)
	v_mul_f32_e32 v6, 0x43800000, v26
	v_med3_f32 v6, v6, s54, v192
	v_cvt_pk_fp8_f32 v68, v2, v6
	s_waitcnt vmcnt(5)
	v_mul_f32_e32 v14, 0x43800000, v42
	v_med3_f32 v14, v14, s54, v192
	s_waitcnt vmcnt(4)
	v_mul_f32_e32 v18, 0x43800000, v62
	v_med3_f32 v18, v18, s54, v192
	v_cvt_pk_fp8_f32 v68, v14, v18 op_sel:[0,0,1]
	s_waitcnt vmcnt(3)
	v_mul_f32_e32 v2, 0x43800000, v10
	v_med3_f32 v2, v2, s54, v192
	s_waitcnt vmcnt(2)
	v_mul_f32_e32 v6, 0x43800000, v30
	v_med3_f32 v6, v6, s54, v192
	v_cvt_pk_fp8_f32 v69, v2, v6
	v_mul_u32_u24_e32 v2, 0x110, v71
	v_add3_u32 v6, s2, v70, v2
	v_mul_f32_e32 v2, 0x43800000, v15
	s_waitcnt vmcnt(1)
	v_mul_f32_e32 v10, 0x43800000, v46
	v_med3_f32 v10, v10, s54, v192
	v_med3_f32 v2, v2, s54, v192
	s_waitcnt vmcnt(0)
	v_mul_f32_e32 v14, 0x43800000, v50
	v_med3_f32 v14, v14, s54, v192
	v_cvt_pk_fp8_f32 v69, v10, v14 op_sel:[0,0,1]
	v_mul_f32_e32 v10, 0x43800000, v19
	v_med3_f32 v10, v10, s54, v192
	v_mul_f32_e32 v14, 0x43800000, v35
	ds_write_b128 v6, v[66:69]
	v_mov_b32_e32 v66, v163
	v_cvt_pk_fp8_f32 v66, v2, v10
	v_mul_f32_e32 v2, 0x43800000, v3
	v_mul_f32_e32 v3, 0x43800000, v23
	v_med3_f32 v2, v2, s54, v192
	v_med3_f32 v3, v3, s54, v192
	v_mov_b32_e32 v67, v163
	v_mul_f32_e32 v15, 0x43800000, v55
	v_cvt_pk_fp8_f32 v67, v2, v3
	v_mul_f32_e32 v2, 0x43800000, v7
	v_mul_f32_e32 v3, 0x43800000, v27
	v_med3_f32 v14, v14, s54, v192
	v_med3_f32 v15, v15, s54, v192
	v_med3_f32 v2, v2, s54, v192
	v_med3_f32 v3, v3, s54, v192
	v_mov_b32_e32 v68, v163
	v_cvt_pk_fp8_f32 v66, v14, v15 op_sel:[0,0,1]
	v_mul_f32_e32 v10, 0x43800000, v39
	v_mul_f32_e32 v14, 0x43800000, v59
	v_cvt_pk_fp8_f32 v68, v2, v3
	v_mul_f32_e32 v2, 0x43800000, v11
	v_mul_f32_e32 v3, 0x43800000, v31
	v_med3_f32 v10, v10, s54, v192
	v_med3_f32 v14, v14, s54, v192
	v_med3_f32 v2, v2, s54, v192
	v_med3_f32 v3, v3, s54, v192
	v_mov_b32_e32 v69, v163
	v_cvt_pk_fp8_f32 v67, v10, v14 op_sel:[0,0,1]
	v_mul_f32_e32 v7, 0x43800000, v43
	v_mul_f32_e32 v10, 0x43800000, v63
	v_cvt_pk_fp8_f32 v69, v2, v3
	v_med3_f32 v7, v7, s54, v192
	v_med3_f32 v10, v10, s54, v192
	v_cvt_pk_fp8_f32 v68, v7, v10 op_sel:[0,0,1]
	v_mul_f32_e32 v7, 0x43800000, v47
	v_mul_f32_e32 v10, 0x43800000, v51
	v_med3_f32 v7, v7, s54, v192
	v_med3_f32 v10, v10, s54, v192
	v_cvt_pk_fp8_f32 v69, v7, v10 op_sel:[0,0,1]
	v_mul_f32_e32 v2, 0x43800000, v16
	v_mul_f32_e32 v3, 0x43800000, v20
	v_med3_f32 v2, v2, s54, v192
	ds_write_b128 v6, v[66:69] offset:272
	v_med3_f32 v3, v3, s54, v192
	v_mov_b32_e32 v66, v163
	v_cvt_pk_fp8_f32 v66, v2, v3
	v_mul_f32_e32 v2, 0x43800000, v4
	v_mul_f32_e32 v3, 0x43800000, v24
	v_med3_f32 v2, v2, s54, v192
	v_med3_f32 v3, v3, s54, v192
	v_mov_b32_e32 v67, v163
	v_mul_f32_e32 v7, 0x43800000, v36
	v_mul_f32_e32 v10, 0x43800000, v56
	v_cvt_pk_fp8_f32 v67, v2, v3
	v_mul_f32_e32 v2, 0x43800000, v8
	v_mul_f32_e32 v3, 0x43800000, v28
	v_med3_f32 v7, v7, s54, v192
	v_med3_f32 v10, v10, s54, v192
	v_med3_f32 v2, v2, s54, v192
	v_med3_f32 v3, v3, s54, v192
	v_mov_b32_e32 v68, v163
	v_cvt_pk_fp8_f32 v66, v7, v10 op_sel:[0,0,1]
	v_mul_f32_e32 v4, 0x43800000, v40
	v_mul_f32_e32 v7, 0x43800000, v60
	v_cvt_pk_fp8_f32 v68, v2, v3
	v_mul_f32_e32 v2, 0x43800000, v12
	v_mul_f32_e32 v3, 0x43800000, v32
	v_med3_f32 v4, v4, s54, v192
	v_med3_f32 v7, v7, s54, v192
	v_med3_f32 v2, v2, s54, v192
	v_med3_f32 v3, v3, s54, v192
	v_mov_b32_e32 v69, v163
	v_cvt_pk_fp8_f32 v67, v4, v7 op_sel:[0,0,1]
	v_mul_f32_e32 v4, 0x43800000, v44
	v_mul_f32_e32 v7, 0x43800000, v64
	v_cvt_pk_fp8_f32 v69, v2, v3
	v_mul_f32_e32 v2, 0x43800000, v17
	v_mul_f32_e32 v3, 0x43800000, v21
	v_med3_f32 v4, v4, s54, v192
	v_med3_f32 v7, v7, s54, v192
	v_med3_f32 v8, v2, s54, v192
	v_med3_f32 v3, v3, s54, v192
	v_mov_b32_e32 v2, v163
	v_cvt_pk_fp8_f32 v68, v4, v7 op_sel:[0,0,1]
	v_mul_f32_e32 v4, 0x43800000, v48
	v_mul_f32_e32 v7, 0x43800000, v52
	v_cvt_pk_fp8_f32 v2, v8, v3
	v_med3_f32 v4, v4, s54, v192
	v_med3_f32 v7, v7, s54, v192
	v_cvt_pk_fp8_f32 v69, v4, v7 op_sel:[0,0,1]
	v_mul_f32_e32 v4, 0x43800000, v37
	v_mul_f32_e32 v7, 0x43800000, v57
	v_med3_f32 v4, v4, s54, v192
	v_med3_f32 v7, v7, s54, v192
	v_cvt_pk_fp8_f32 v2, v4, v7 op_sel:[0,0,1]
	v_mul_f32_e32 v3, 0x43800000, v5
	v_mul_f32_e32 v4, 0x43800000, v25
	v_med3_f32 v8, v3, s54, v192
	v_med3_f32 v4, v4, s54, v192
	v_mov_b32_e32 v3, v163
	v_cvt_pk_fp8_f32 v3, v8, v4
	v_mul_f32_e32 v5, 0x43800000, v41
	v_mul_f32_e32 v7, 0x43800000, v61
	v_med3_f32 v5, v5, s54, v192
	v_med3_f32 v7, v7, s54, v192
	v_cvt_pk_fp8_f32 v3, v5, v7 op_sel:[0,0,1]
	v_mul_f32_e32 v4, 0x43800000, v9
	v_mul_f32_e32 v5, 0x43800000, v29
	v_med3_f32 v9, v4, s54, v192
	v_med3_f32 v5, v5, s54, v192
	v_mov_b32_e32 v4, v163
	v_cvt_pk_fp8_f32 v4, v9, v5
	v_mul_f32_e32 v7, 0x43800000, v45
	v_mul_f32_e32 v8, 0x43800000, v65
	v_med3_f32 v7, v7, s54, v192
	v_med3_f32 v8, v8, s54, v192
	v_cvt_pk_fp8_f32 v4, v7, v8 op_sel:[0,0,1]
	v_mul_f32_e32 v5, 0x43800000, v13
	v_mul_f32_e32 v7, 0x43800000, v33
	v_med3_f32 v10, v5, s54, v192
	v_med3_f32 v7, v7, s54, v192
	v_mov_b32_e32 v5, v163
	v_cvt_pk_fp8_f32 v5, v10, v7
	v_mul_f32_e32 v8, 0x43800000, v49
	v_mul_f32_e32 v9, 0x43800000, v53
	v_med3_f32 v8, v8, s54, v192
	v_med3_f32 v9, v9, s54, v192
	v_cvt_pk_fp8_f32 v5, v8, v9 op_sel:[0,0,1]
	ds_write_b128 v6, v[66:69] offset:544
	v_ashrrev_i32_e32 v10, 4, v1
	v_ashrrev_i32_e32 v11, 31, v10
	ds_write_b128 v6, v[2:5] offset:816
	v_lshlrev_b32_e32 v2, 4, v1
	v_and_b32_e32 v162, 0xf0, v2
	v_add_u32_e32 v6, 0, v162
	v_lshl_add_u64 v[8:9], s[10:11], 0, v[162:163]
	v_mad_u64_u32 v[2:3], s[10:11], v10, s55, v[6:7]
	s_waitcnt lgkmcnt(0)
	s_barrier
	ds_read_b128 v[2:5], v2
	v_lshlrev_b64 v[10:11], 11, v[10:11]
	v_lshl_add_u64 v[10:11], v[8:9], 0, v[10:11]
	s_waitcnt lgkmcnt(0)
	global_store_dwordx4 v[10:11], v[2:5], off
	s_nop 1
	v_add_u32_e32 v2, 0x200, v1
	v_ashrrev_i32_e32 v10, 4, v2
	v_mad_u64_u32 v[2:3], s[10:11], v10, s55, v[6:7]
	ds_read_b128 v[2:5], v2
	v_ashrrev_i32_e32 v11, 31, v10
	v_lshlrev_b64 v[10:11], 11, v[10:11]
	v_lshl_add_u64 v[10:11], v[8:9], 0, v[10:11]
	s_waitcnt lgkmcnt(0)
	global_store_dwordx4 v[10:11], v[2:5], off
	s_nop 1
	v_add_u32_e32 v2, 0x400, v1
	v_ashrrev_i32_e32 v10, 4, v2
	v_mad_u64_u32 v[2:3], s[10:11], v10, s55, v[6:7]
	ds_read_b128 v[2:5], v2
	v_ashrrev_i32_e32 v11, 31, v10
	v_lshlrev_b64 v[10:11], 11, v[10:11]
	v_lshl_add_u64 v[10:11], v[8:9], 0, v[10:11]
	v_add_u32_e32 v1, 0x600, v1
	s_waitcnt lgkmcnt(0)
	global_store_dwordx4 v[10:11], v[2:5], off
	v_ashrrev_i32_e32 v10, 4, v1
	v_ashrrev_i32_e32 v11, 31, v10
	v_mad_u64_u32 v[2:3], s[10:11], v10, s55, v[6:7]
	ds_read_b128 v[2:5], v2
	v_lshlrev_b64 v[6:7], 11, v[10:11]
	v_lshl_add_u64 v[6:7], v[8:9], 0, v[6:7]
	s_waitcnt lgkmcnt(0)
	global_store_dwordx4 v[6:7], v[2:5], off
	s_barrier

.LBB0_953:
	s_cmp_lt_i32 s96, 6
	s_cselect_b64 s[0:1], -1, 0
	s_and_b64 s[8:9], s[0:1], s[6:7]
	s_andn2_b64 vcc, exec, s[8:9]
	s_cbranch_vccnz .LBB0_996
	v_readlane_b32 s2, v254, 55
	s_bitcmp1_b32 s74, 3
	v_readlane_b32 s3, v254, 56
	s_cselect_b64 s[0:1], -1, 0
	s_xor_b64 s[10:11], s[2:3], -1
	s_or_b64 s[0:1], s[0:1], s[10:11]
	s_mov_b64 s[6:7], -1
	s_and_b64 vcc, exec, s[0:1]
	s_cbranch_vccnz .LBB0_960
	s_barrier
	s_add_u32 s5, s74, 768
	s_lshr_b32 s4, s5, 5
	s_and_b32 s5, s5, 31
	v_readlane_b32 s0, v254, 6
	v_readlane_b32 s1, v254, 7
	s_lshl_b32 s6, s4, 25
	s_and_b32 s7, s5, 1
	s_lshl_b32 s7, s7, 13
	s_add_u32 s6, s6, s7
	s_lshr_b32 s7, s5, 1
	s_lshl_b32 s7, s7, 9
	s_add_u32 s6, s6, s7
	s_add_u32 s0, s0, s6
	s_addc_u32 s1, s1, 0
	s_lshl_b32 s6, s4, 23
	s_lshl_b32 s7, s5, 18
	s_add_u32 s6, s6, s7
	s_add_u32 s6, s6, 0x40000000
	s_add_u32 s2, s78, s6
	s_addc_u32 s3, s79, 0
	s_mov_b32 s6, 0xc3e00000
	v_mov_b32_e32 v1, 0x43e00000
	v_lshrrev_b32_e32 v226, 5, v0
	v_and_b32_e32 v227, 31, v0
	v_lshlrev_b32_e32 v228, 4, v227
	v_lshlrev_b32_e32 v229, 18, v226
	v_add_u32_e32 v250, v229, v228
	v_add_u32_e32 v251, 0x4000, v250
	v_add_u32_e32 v246, 0x8000, v250
	v_add_u32_e32 v247, 0xc000, v250
	v_add_u32_e32 v248, 0x10000, v250
	v_add_u32_e32 v249, 0x14000, v250
	v_add_u32_e32 v242, 0x18000, v250
	v_add_u32_e32 v243, 0x1c000, v250
	v_add_u32_e32 v244, 0x20000, v250
	v_add_u32_e32 v245, 0x24000, v250
	v_add_u32_e32 v238, 0x28000, v250
	v_add_u32_e32 v239, 0x2c000, v250
	v_add_u32_e32 v240, 0x30000, v250
	v_add_u32_e32 v241, 0x34000, v250
	v_add_u32_e32 v234, 0x38000, v250
	v_add_u32_e32 v235, 0x3c000, v250
	v_lshrrev_b32_e32 v194, 4, v0
	v_and_b32_e32 v195, 15, v0
	v_lshlrev_b32_e32 v236, 11, v194
	v_lshl_add_u32 v236, v195, 4, v236
	v_add_u32_e32 v237, 0x10000, v236
	v_add_u32_e32 v230, 0x20000, v236
	v_add_u32_e32 v231, 0x30000, v236
	v_mul_u32_u24_e32 v232, 0x440, v227
	v_lshl_add_u32 v232, v226, 4, v232
	v_mul_u32_u24_e32 v233, 0x110, v194
	v_lshl_add_u32 v233, v195, 4, v233
	global_load_dwordx4 v[2:5], v250, s[0:1] sc0 nt
	global_load_dwordx4 v[6:9], v251, s[0:1] sc0 nt
	global_load_dwordx4 v[10:13], v246, s[0:1] sc0 nt
	global_load_dwordx4 v[14:17], v247, s[0:1] sc0 nt
	global_load_dwordx4 v[18:21], v248, s[0:1] sc0 nt
	global_load_dwordx4 v[22:25], v249, s[0:1] sc0 nt
	global_load_dwordx4 v[26:29], v242, s[0:1] sc0 nt
	global_load_dwordx4 v[30:33], v243, s[0:1] sc0 nt
	global_load_dwordx4 v[34:37], v244, s[0:1] sc0 nt
	global_load_dwordx4 v[38:41], v245, s[0:1] sc0 nt
	global_load_dwordx4 v[42:45], v238, s[0:1] sc0 nt
	global_load_dwordx4 v[46:49], v239, s[0:1] sc0 nt
	global_load_dwordx4 v[50:53], v240, s[0:1] sc0 nt
	global_load_dwordx4 v[54:57], v241, s[0:1] sc0 nt
	global_load_dwordx4 v[58:61], v234, s[0:1] sc0 nt
	global_load_dwordx4 v[62:65], v235, s[0:1] sc0 nt
	s_add_u32 s0, s0, 0x400000
	s_addc_u32 s1, s1, 0
	global_load_dwordx4 v[66:69], v250, s[0:1] sc0 nt
	global_load_dwordx4 v[70:73], v251, s[0:1] sc0 nt
	global_load_dwordx4 v[74:77], v246, s[0:1] sc0 nt
	global_load_dwordx4 v[78:81], v247, s[0:1] sc0 nt
	global_load_dwordx4 v[82:85], v248, s[0:1] sc0 nt
	global_load_dwordx4 v[86:89], v249, s[0:1] sc0 nt
	global_load_dwordx4 v[90:93], v242, s[0:1] sc0 nt
	global_load_dwordx4 v[94:97], v243, s[0:1] sc0 nt
	global_load_dwordx4 v[98:101], v244, s[0:1] sc0 nt
	global_load_dwordx4 v[102:105], v245, s[0:1] sc0 nt
	global_load_dwordx4 v[106:109], v238, s[0:1] sc0 nt
	global_load_dwordx4 v[110:113], v239, s[0:1] sc0 nt
	global_load_dwordx4 v[114:117], v240, s[0:1] sc0 nt
	global_load_dwordx4 v[118:121], v241, s[0:1] sc0 nt
	global_load_dwordx4 v[122:125], v234, s[0:1] sc0 nt
	global_load_dwordx4 v[126:129], v235, s[0:1] sc0 nt
	s_add_u32 s0, s0, 0x400000
	s_addc_u32 s1, s1, 0
	global_load_dwordx4 v[130:133], v250, s[0:1] sc0 nt
	global_load_dwordx4 v[134:137], v251, s[0:1] sc0 nt
	global_load_dwordx4 v[138:141], v246, s[0:1] sc0 nt
	global_load_dwordx4 v[142:145], v247, s[0:1] sc0 nt
	global_load_dwordx4 v[146:149], v248, s[0:1] sc0 nt
	global_load_dwordx4 v[150:153], v249, s[0:1] sc0 nt
	global_load_dwordx4 v[154:157], v242, s[0:1] sc0 nt
	global_load_dwordx4 v[158:161], v243, s[0:1] sc0 nt
	global_load_dwordx4 v[162:165], v244, s[0:1] sc0 nt
	global_load_dwordx4 v[166:169], v245, s[0:1] sc0 nt
	global_load_dwordx4 v[170:173], v238, s[0:1] sc0 nt
	global_load_dwordx4 v[174:177], v239, s[0:1] sc0 nt
	global_load_dwordx4 v[178:181], v240, s[0:1] sc0 nt
	global_load_dwordx4 v[182:185], v241, s[0:1] sc0 nt
	global_load_dwordx4 v[186:189], v234, s[0:1] sc0 nt
	global_load_dwordx4 v[190:193], v235, s[0:1] sc0 nt
	s_add_u32 s0, s0, 0x400000
	s_addc_u32 s1, s1, 0
	s_waitcnt vmcnt(44)
	v_mul_f32_e32 v226, 0x43800000, v2
	v_mul_f32_e32 v227, 0x43800000, v6
	v_med3_f32 v226, v226, s6, v1
	v_med3_f32 v227, v227, s6, v1
	v_mul_f32_e32 v228, 0x43800000, v10
	v_mul_f32_e32 v229, 0x43800000, v14
	v_cvt_pk_fp8_f32 v194, v226, v227
	v_med3_f32 v228, v228, s6, v1
	v_med3_f32 v229, v229, s6, v1
	v_cvt_pk_fp8_f32 v194, v228, v229 op_sel:[0,0,1]
	s_waitcnt vmcnt(40)
	v_mul_f32_e32 v226, 0x43800000, v18
	v_mul_f32_e32 v227, 0x43800000, v22
	v_med3_f32 v226, v226, s6, v1
	v_med3_f32 v227, v227, s6, v1
	v_mul_f32_e32 v228, 0x43800000, v26
	v_mul_f32_e32 v229, 0x43800000, v30
	v_cvt_pk_fp8_f32 v195, v226, v227
	v_med3_f32 v228, v228, s6, v1
	v_med3_f32 v229, v229, s6, v1
	v_cvt_pk_fp8_f32 v195, v228, v229 op_sel:[0,0,1]
	s_waitcnt vmcnt(36)
	v_mul_f32_e32 v226, 0x43800000, v34
	v_mul_f32_e32 v227, 0x43800000, v38
	v_med3_f32 v226, v226, s6, v1
	v_med3_f32 v227, v227, s6, v1
	v_mul_f32_e32 v228, 0x43800000, v42
	v_mul_f32_e32 v229, 0x43800000, v46
	v_cvt_pk_fp8_f32 v196, v226, v227
	v_med3_f32 v228, v228, s6, v1
	v_med3_f32 v229, v229, s6, v1
	v_cvt_pk_fp8_f32 v196, v228, v229 op_sel:[0,0,1]
	s_waitcnt vmcnt(32)
	v_mul_f32_e32 v226, 0x43800000, v50
	v_mul_f32_e32 v227, 0x43800000, v54
	v_med3_f32 v226, v226, s6, v1
	v_med3_f32 v227, v227, s6, v1
	v_mul_f32_e32 v228, 0x43800000, v58
	v_mul_f32_e32 v229, 0x43800000, v62
	v_cvt_pk_fp8_f32 v197, v226, v227
	v_med3_f32 v228, v228, s6, v1
	v_med3_f32 v229, v229, s6, v1
	v_cvt_pk_fp8_f32 v197, v228, v229 op_sel:[0,0,1]
	s_nop 1
	ds_write_b128 v232, v[194:197] offset:0
	v_mul_f32_e32 v226, 0x43800000, v3
	v_mul_f32_e32 v227, 0x43800000, v7
	v_med3_f32 v226, v226, s6, v1
	v_med3_f32 v227, v227, s6, v1
	v_mul_f32_e32 v228, 0x43800000, v11
	v_mul_f32_e32 v229, 0x43800000, v15
	v_cvt_pk_fp8_f32 v198, v226, v227
	v_med3_f32 v228, v228, s6, v1
	v_med3_f32 v229, v229, s6, v1
	v_cvt_pk_fp8_f32 v198, v228, v229 op_sel:[0,0,1]
	v_mul_f32_e32 v226, 0x43800000, v19
	v_mul_f32_e32 v227, 0x43800000, v23
	v_med3_f32 v226, v226, s6, v1
	v_med3_f32 v227, v227, s6, v1
	v_mul_f32_e32 v228, 0x43800000, v27
	v_mul_f32_e32 v229, 0x43800000, v31
	v_cvt_pk_fp8_f32 v199, v226, v227
	v_med3_f32 v228, v228, s6, v1
	v_med3_f32 v229, v229, s6, v1
	v_cvt_pk_fp8_f32 v199, v228, v229 op_sel:[0,0,1]
	v_mul_f32_e32 v226, 0x43800000, v35
	v_mul_f32_e32 v227, 0x43800000, v39
	v_med3_f32 v226, v226, s6, v1
	v_med3_f32 v227, v227, s6, v1
	v_mul_f32_e32 v228, 0x43800000, v43
	v_mul_f32_e32 v229, 0x43800000, v47
	v_cvt_pk_fp8_f32 v200, v226, v227
	v_med3_f32 v228, v228, s6, v1
	v_med3_f32 v229, v229, s6, v1
	v_cvt_pk_fp8_f32 v200, v228, v229 op_sel:[0,0,1]
	v_mul_f32_e32 v226, 0x43800000, v51
	v_mul_f32_e32 v227, 0x43800000, v55
	v_med3_f32 v226, v226, s6, v1
	v_med3_f32 v227, v227, s6, v1
	v_mul_f32_e32 v228, 0x43800000, v59
	v_mul_f32_e32 v229, 0x43800000, v63
	v_cvt_pk_fp8_f32 v201, v226, v227
	v_med3_f32 v228, v228, s6, v1
	v_med3_f32 v229, v229, s6, v1
	v_cvt_pk_fp8_f32 v201, v228, v229 op_sel:[0,0,1]
	s_nop 1
	ds_write_b128 v232, v[198:201] offset:272
	v_mul_f32_e32 v226, 0x43800000, v4
	v_mul_f32_e32 v227, 0x43800000, v8
	v_med3_f32 v226, v226, s6, v1
	v_med3_f32 v227, v227, s6, v1
	v_mul_f32_e32 v228, 0x43800000, v12
	v_mul_f32_e32 v229, 0x43800000, v16
	v_cvt_pk_fp8_f32 v202, v226, v227
	v_med3_f32 v228, v228, s6, v1
	v_med3_f32 v229, v229, s6, v1
	v_cvt_pk_fp8_f32 v202, v228, v229 op_sel:[0,0,1]
	v_mul_f32_e32 v226, 0x43800000, v20
	v_mul_f32_e32 v227, 0x43800000, v24
	v_med3_f32 v226, v226, s6, v1
	v_med3_f32 v227, v227, s6, v1
	v_mul_f32_e32 v228, 0x43800000, v28
	v_mul_f32_e32 v229, 0x43800000, v32
	v_cvt_pk_fp8_f32 v203, v226, v227
	v_med3_f32 v228, v228, s6, v1
	v_med3_f32 v229, v229, s6, v1
	v_cvt_pk_fp8_f32 v203, v228, v229 op_sel:[0,0,1]
	v_mul_f32_e32 v226, 0x43800000, v36
	v_mul_f32_e32 v227, 0x43800000, v40
	v_med3_f32 v226, v226, s6, v1
	v_med3_f32 v227, v227, s6, v1
	v_mul_f32_e32 v228, 0x43800000, v44
	v_mul_f32_e32 v229, 0x43800000, v48
	v_cvt_pk_fp8_f32 v204, v226, v227
	v_med3_f32 v228, v228, s6, v1
	v_med3_f32 v229, v229, s6, v1
	v_cvt_pk_fp8_f32 v204, v228, v229 op_sel:[0,0,1]
	v_mul_f32_e32 v226, 0x43800000, v52
	v_mul_f32_e32 v227, 0x43800000, v56
	v_med3_f32 v226, v226, s6, v1
	v_med3_f32 v227, v227, s6, v1
	v_mul_f32_e32 v228, 0x43800000, v60
	v_mul_f32_e32 v229, 0x43800000, v64
	v_cvt_pk_fp8_f32 v205, v226, v227
	v_med3_f32 v228, v228, s6, v1
	v_med3_f32 v229, v229, s6, v1
	v_cvt_pk_fp8_f32 v205, v228, v229 op_sel:[0,0,1]
	s_nop 1
	ds_write_b128 v232, v[202:205] offset:544
	v_mul_f32_e32 v226, 0x43800000, v5
	v_mul_f32_e32 v227, 0x43800000, v9
	v_med3_f32 v226, v226, s6, v1
	v_med3_f32 v227, v227, s6, v1
	v_mul_f32_e32 v228, 0x43800000, v13
	v_mul_f32_e32 v229, 0x43800000, v17
	v_cvt_pk_fp8_f32 v206, v226, v227
	v_med3_f32 v228, v228, s6, v1
	v_med3_f32 v229, v229, s6, v1
	v_cvt_pk_fp8_f32 v206, v228, v229 op_sel:[0,0,1]
	v_mul_f32_e32 v226, 0x43800000, v21
	v_mul_f32_e32 v227, 0x43800000, v25
	v_med3_f32 v226, v226, s6, v1
	v_med3_f32 v227, v227, s6, v1
	v_mul_f32_e32 v228, 0x43800000, v29
	v_mul_f32_e32 v229, 0x43800000, v33
	v_cvt_pk_fp8_f32 v207, v226, v227
	v_med3_f32 v228, v228, s6, v1
	v_med3_f32 v229, v229, s6, v1
	v_cvt_pk_fp8_f32 v207, v228, v229 op_sel:[0,0,1]
	v_mul_f32_e32 v226, 0x43800000, v37
	v_mul_f32_e32 v227, 0x43800000, v41
	v_med3_f32 v226, v226, s6, v1
	v_med3_f32 v227, v227, s6, v1
	v_mul_f32_e32 v228, 0x43800000, v45
	v_mul_f32_e32 v229, 0x43800000, v49
	v_cvt_pk_fp8_f32 v208, v226, v227
	v_med3_f32 v228, v228, s6, v1
	v_med3_f32 v229, v229, s6, v1
	v_cvt_pk_fp8_f32 v208, v228, v229 op_sel:[0,0,1]
	v_mul_f32_e32 v226, 0x43800000, v53
	v_mul_f32_e32 v227, 0x43800000, v57
	v_med3_f32 v226, v226, s6, v1
	v_med3_f32 v227, v227, s6, v1
	v_mul_f32_e32 v228, 0x43800000, v61
	v_mul_f32_e32 v229, 0x43800000, v65
	v_cvt_pk_fp8_f32 v209, v226, v227
	v_med3_f32 v228, v228, s6, v1
	v_med3_f32 v229, v229, s6, v1
	v_cvt_pk_fp8_f32 v209, v228, v229 op_sel:[0,0,1]
	s_nop 1
	ds_write_b128 v232, v[206:209] offset:816
	s_waitcnt lgkmcnt(0)
	s_barrier
	global_load_dwordx4 v[2:5], v250, s[0:1] sc0 nt
	global_load_dwordx4 v[6:9], v251, s[0:1] sc0 nt
	global_load_dwordx4 v[10:13], v246, s[0:1] sc0 nt
	global_load_dwordx4 v[14:17], v247, s[0:1] sc0 nt
	global_load_dwordx4 v[18:21], v248, s[0:1] sc0 nt
	global_load_dwordx4 v[22:25], v249, s[0:1] sc0 nt
	global_load_dwordx4 v[26:29], v242, s[0:1] sc0 nt
	global_load_dwordx4 v[30:33], v243, s[0:1] sc0 nt
	global_load_dwordx4 v[34:37], v244, s[0:1] sc0 nt
	global_load_dwordx4 v[38:41], v245, s[0:1] sc0 nt
	global_load_dwordx4 v[42:45], v238, s[0:1] sc0 nt
	global_load_dwordx4 v[46:49], v239, s[0:1] sc0 nt
	global_load_dwordx4 v[50:53], v240, s[0:1] sc0 nt
	global_load_dwordx4 v[54:57], v241, s[0:1] sc0 nt
	global_load_dwordx4 v[58:61], v234, s[0:1] sc0 nt
	global_load_dwordx4 v[62:65], v235, s[0:1] sc0 nt
	s_add_u32 s0, s0, 0x400000
	s_addc_u32 s1, s1, 0
	ds_read_b128 v[194:197], v233 offset:0
	ds_read_b128 v[198:201], v233 offset:8704
	ds_read_b128 v[202:205], v233 offset:17408
	ds_read_b128 v[206:209], v233 offset:26112
	s_waitcnt lgkmcnt(3)
	global_store_dwordx4 v236, v[194:197], s[2:3] nt
	s_waitcnt lgkmcnt(2)
	global_store_dwordx4 v237, v[198:201], s[2:3] nt
	s_waitcnt lgkmcnt(1)
	global_store_dwordx4 v230, v[202:205], s[2:3] nt
	s_waitcnt lgkmcnt(0)
	global_store_dwordx4 v231, v[206:209], s[2:3] nt
	s_add_u32 s2, s2, 0x100
	s_addc_u32 s3, s3, 0
	s_waitcnt vmcnt(48)
	v_mul_f32_e32 v226, 0x43800000, v66
	v_mul_f32_e32 v227, 0x43800000, v70
	v_med3_f32 v226, v226, s6, v1
	v_med3_f32 v227, v227, s6, v1
	v_mul_f32_e32 v228, 0x43800000, v74
	v_mul_f32_e32 v229, 0x43800000, v78
	v_cvt_pk_fp8_f32 v194, v226, v227
	v_med3_f32 v228, v228, s6, v1
	v_med3_f32 v229, v229, s6, v1
	v_cvt_pk_fp8_f32 v194, v228, v229 op_sel:[0,0,1]
	s_waitcnt vmcnt(44)
	v_mul_f32_e32 v226, 0x43800000, v82
	v_mul_f32_e32 v227, 0x43800000, v86
	v_med3_f32 v226, v226, s6, v1
	v_med3_f32 v227, v227, s6, v1
	v_mul_f32_e32 v228, 0x43800000, v90
	v_mul_f32_e32 v229, 0x43800000, v94
	v_cvt_pk_fp8_f32 v195, v226, v227
	v_med3_f32 v228, v228, s6, v1
	v_med3_f32 v229, v229, s6, v1
	v_cvt_pk_fp8_f32 v195, v228, v229 op_sel:[0,0,1]
	s_waitcnt vmcnt(40)
	v_mul_f32_e32 v226, 0x43800000, v98
	v_mul_f32_e32 v227, 0x43800000, v102
	v_med3_f32 v226, v226, s6, v1
	v_med3_f32 v227, v227, s6, v1
	v_mul_f32_e32 v228, 0x43800000, v106
	v_mul_f32_e32 v229, 0x43800000, v110
	v_cvt_pk_fp8_f32 v196, v226, v227
	v_med3_f32 v228, v228, s6, v1
	v_med3_f32 v229, v229, s6, v1
	v_cvt_pk_fp8_f32 v196, v228, v229 op_sel:[0,0,1]
	s_waitcnt vmcnt(36)
	v_mul_f32_e32 v226, 0x43800000, v114
	v_mul_f32_e32 v227, 0x43800000, v118
	v_med3_f32 v226, v226, s6, v1
	v_med3_f32 v227, v227, s6, v1
	v_mul_f32_e32 v228, 0x43800000, v122
	v_mul_f32_e32 v229, 0x43800000, v126
	v_cvt_pk_fp8_f32 v197, v226, v227
	v_med3_f32 v228, v228, s6, v1
	v_med3_f32 v229, v229, s6, v1
	v_cvt_pk_fp8_f32 v197, v228, v229 op_sel:[0,0,1]
	s_nop 1
	ds_write_b128 v232, v[194:197] offset:34816
	v_mul_f32_e32 v226, 0x43800000, v67
	v_mul_f32_e32 v227, 0x43800000, v71
	v_med3_f32 v226, v226, s6, v1
	v_med3_f32 v227, v227, s6, v1
	v_mul_f32_e32 v228, 0x43800000, v75
	v_mul_f32_e32 v229, 0x43800000, v79
	v_cvt_pk_fp8_f32 v198, v226, v227
	v_med3_f32 v228, v228, s6, v1
	v_med3_f32 v229, v229, s6, v1
	v_cvt_pk_fp8_f32 v198, v228, v229 op_sel:[0,0,1]
	v_mul_f32_e32 v226, 0x43800000, v83
	v_mul_f32_e32 v227, 0x43800000, v87
	v_med3_f32 v226, v226, s6, v1
	v_med3_f32 v227, v227, s6, v1
	v_mul_f32_e32 v228, 0x43800000, v91
	v_mul_f32_e32 v229, 0x43800000, v95
	v_cvt_pk_fp8_f32 v199, v226, v227
	v_med3_f32 v228, v228, s6, v1
	v_med3_f32 v229, v229, s6, v1
	v_cvt_pk_fp8_f32 v199, v228, v229 op_sel:[0,0,1]
	v_mul_f32_e32 v226, 0x43800000, v99
	v_mul_f32_e32 v227, 0x43800000, v103
	v_med3_f32 v226, v226, s6, v1
	v_med3_f32 v227, v227, s6, v1
	v_mul_f32_e32 v228, 0x43800000, v107
	v_mul_f32_e32 v229, 0x43800000, v111
	v_cvt_pk_fp8_f32 v200, v226, v227
	v_med3_f32 v228, v228, s6, v1
	v_med3_f32 v229, v229, s6, v1
	v_cvt_pk_fp8_f32 v200, v228, v229 op_sel:[0,0,1]
	v_mul_f32_e32 v226, 0x43800000, v115
	v_mul_f32_e32 v227, 0x43800000, v119
	v_med3_f32 v226, v226, s6, v1
	v_med3_f32 v227, v227, s6, v1
	v_mul_f32_e32 v228, 0x43800000, v123
	v_mul_f32_e32 v229, 0x43800000, v127
	v_cvt_pk_fp8_f32 v201, v226, v227
	v_med3_f32 v228, v228, s6, v1
	v_med3_f32 v229, v229, s6, v1
	v_cvt_pk_fp8_f32 v201, v228, v229 op_sel:[0,0,1]
	s_nop 1
	ds_write_b128 v232, v[198:201] offset:35088
	v_mul_f32_e32 v226, 0x43800000, v68
	v_mul_f32_e32 v227, 0x43800000, v72
	v_med3_f32 v226, v226, s6, v1
	v_med3_f32 v227, v227, s6, v1
	v_mul_f32_e32 v228, 0x43800000, v76
	v_mul_f32_e32 v229, 0x43800000, v80
	v_cvt_pk_fp8_f32 v202, v226, v227
	v_med3_f32 v228, v228, s6, v1
	v_med3_f32 v229, v229, s6, v1
	v_cvt_pk_fp8_f32 v202, v228, v229 op_sel:[0,0,1]
	v_mul_f32_e32 v226, 0x43800000, v84
	v_mul_f32_e32 v227, 0x43800000, v88
	v_med3_f32 v226, v226, s6, v1
	v_med3_f32 v227, v227, s6, v1
	v_mul_f32_e32 v228, 0x43800000, v92
	v_mul_f32_e32 v229, 0x43800000, v96
	v_cvt_pk_fp8_f32 v203, v226, v227
	v_med3_f32 v228, v228, s6, v1
	v_med3_f32 v229, v229, s6, v1
	v_cvt_pk_fp8_f32 v203, v228, v229 op_sel:[0,0,1]
	v_mul_f32_e32 v226, 0x43800000, v100
	v_mul_f32_e32 v227, 0x43800000, v104
	v_med3_f32 v226, v226, s6, v1
	v_med3_f32 v227, v227, s6, v1
	v_mul_f32_e32 v228, 0x43800000, v108
	v_mul_f32_e32 v229, 0x43800000, v112
	v_cvt_pk_fp8_f32 v204, v226, v227
	v_med3_f32 v228, v228, s6, v1
	v_med3_f32 v229, v229, s6, v1
	v_cvt_pk_fp8_f32 v204, v228, v229 op_sel:[0,0,1]
	v_mul_f32_e32 v226, 0x43800000, v116
	v_mul_f32_e32 v227, 0x43800000, v120
	v_med3_f32 v226, v226, s6, v1
	v_med3_f32 v227, v227, s6, v1
	v_mul_f32_e32 v228, 0x43800000, v124
	v_mul_f32_e32 v229, 0x43800000, v128
	v_cvt_pk_fp8_f32 v205, v226, v227
	v_med3_f32 v228, v228, s6, v1
	v_med3_f32 v229, v229, s6, v1
	v_cvt_pk_fp8_f32 v205, v228, v229 op_sel:[0,0,1]
	s_nop 1
	ds_write_b128 v232, v[202:205] offset:35360
	v_mul_f32_e32 v226, 0x43800000, v69
	v_mul_f32_e32 v227, 0x43800000, v73
	v_med3_f32 v226, v226, s6, v1
	v_med3_f32 v227, v227, s6, v1
	v_mul_f32_e32 v228, 0x43800000, v77
	v_mul_f32_e32 v229, 0x43800000, v81
	v_cvt_pk_fp8_f32 v206, v226, v227
	v_med3_f32 v228, v228, s6, v1
	v_med3_f32 v229, v229, s6, v1
	v_cvt_pk_fp8_f32 v206, v228, v229 op_sel:[0,0,1]
	v_mul_f32_e32 v226, 0x43800000, v85
	v_mul_f32_e32 v227, 0x43800000, v89
	v_med3_f32 v226, v226, s6, v1
	v_med3_f32 v227, v227, s6, v1
	v_mul_f32_e32 v228, 0x43800000, v93
	v_mul_f32_e32 v229, 0x43800000, v97
	v_cvt_pk_fp8_f32 v207, v226, v227
	v_med3_f32 v228, v228, s6, v1
	v_med3_f32 v229, v229, s6, v1
	v_cvt_pk_fp8_f32 v207, v228, v229 op_sel:[0,0,1]
	v_mul_f32_e32 v226, 0x43800000, v101
	v_mul_f32_e32 v227, 0x43800000, v105
	v_med3_f32 v226, v226, s6, v1
	v_med3_f32 v227, v227, s6, v1
	v_mul_f32_e32 v228, 0x43800000, v109
	v_mul_f32_e32 v229, 0x43800000, v113
	v_cvt_pk_fp8_f32 v208, v226, v227
	v_med3_f32 v228, v228, s6, v1
	v_med3_f32 v229, v229, s6, v1
	v_cvt_pk_fp8_f32 v208, v228, v229 op_sel:[0,0,1]
	v_mul_f32_e32 v226, 0x43800000, v117
	v_mul_f32_e32 v227, 0x43800000, v121
	v_med3_f32 v226, v226, s6, v1
	v_med3_f32 v227, v227, s6, v1
	v_mul_f32_e32 v228, 0x43800000, v125
	v_mul_f32_e32 v229, 0x43800000, v129
	v_cvt_pk_fp8_f32 v209, v226, v227
	v_med3_f32 v228, v228, s6, v1
	v_med3_f32 v229, v229, s6, v1
	v_cvt_pk_fp8_f32 v209, v228, v229 op_sel:[0,0,1]
	s_nop 1
	ds_write_b128 v232, v[206:209] offset:35632
	s_waitcnt lgkmcnt(0)
	s_barrier
	global_load_dwordx4 v[66:69], v250, s[0:1] sc0 nt
	global_load_dwordx4 v[70:73], v251, s[0:1] sc0 nt
	global_load_dwordx4 v[74:77], v246, s[0:1] sc0 nt
	global_load_dwordx4 v[78:81], v247, s[0:1] sc0 nt
	global_load_dwordx4 v[82:85], v248, s[0:1] sc0 nt
	global_load_dwordx4 v[86:89], v249, s[0:1] sc0 nt
	global_load_dwordx4 v[90:93], v242, s[0:1] sc0 nt
	global_load_dwordx4 v[94:97], v243, s[0:1] sc0 nt
	global_load_dwordx4 v[98:101], v244, s[0:1] sc0 nt
	global_load_dwordx4 v[102:105], v245, s[0:1] sc0 nt
	global_load_dwordx4 v[106:109], v238, s[0:1] sc0 nt
	global_load_dwordx4 v[110:113], v239, s[0:1] sc0 nt
	global_load_dwordx4 v[114:117], v240, s[0:1] sc0 nt
	global_load_dwordx4 v[118:121], v241, s[0:1] sc0 nt
	global_load_dwordx4 v[122:125], v234, s[0:1] sc0 nt
	global_load_dwordx4 v[126:129], v235, s[0:1] sc0 nt
	s_add_u32 s0, s0, 0x400000
	s_addc_u32 s1, s1, 0
	ds_read_b128 v[194:197], v233 offset:34816
	ds_read_b128 v[198:201], v233 offset:43520
	ds_read_b128 v[202:205], v233 offset:52224
	ds_read_b128 v[206:209], v233 offset:60928
	s_waitcnt lgkmcnt(3)
	global_store_dwordx4 v236, v[194:197], s[2:3] nt
	s_waitcnt lgkmcnt(2)
	global_store_dwordx4 v237, v[198:201], s[2:3] nt
	s_waitcnt lgkmcnt(1)
	global_store_dwordx4 v230, v[202:205], s[2:3] nt
	s_waitcnt lgkmcnt(0)
	global_store_dwordx4 v231, v[206:209], s[2:3] nt
	s_add_u32 s2, s2, 0x100
	s_addc_u32 s3, s3, 0
	s_waitcnt vmcnt(52)
	v_mul_f32_e32 v226, 0x43800000, v130
	v_mul_f32_e32 v227, 0x43800000, v134
	v_med3_f32 v226, v226, s6, v1
	v_med3_f32 v227, v227, s6, v1
	v_mul_f32_e32 v228, 0x43800000, v138
	v_mul_f32_e32 v229, 0x43800000, v142
	v_cvt_pk_fp8_f32 v194, v226, v227
	v_med3_f32 v228, v228, s6, v1
	v_med3_f32 v229, v229, s6, v1
	v_cvt_pk_fp8_f32 v194, v228, v229 op_sel:[0,0,1]
	s_waitcnt vmcnt(48)
	v_mul_f32_e32 v226, 0x43800000, v146
	v_mul_f32_e32 v227, 0x43800000, v150
	v_med3_f32 v226, v226, s6, v1
	v_med3_f32 v227, v227, s6, v1
	v_mul_f32_e32 v228, 0x43800000, v154
	v_mul_f32_e32 v229, 0x43800000, v158
	v_cvt_pk_fp8_f32 v195, v226, v227
	v_med3_f32 v228, v228, s6, v1
	v_med3_f32 v229, v229, s6, v1
	v_cvt_pk_fp8_f32 v195, v228, v229 op_sel:[0,0,1]
	s_waitcnt vmcnt(44)
	v_mul_f32_e32 v226, 0x43800000, v162
	v_mul_f32_e32 v227, 0x43800000, v166
	v_med3_f32 v226, v226, s6, v1
	v_med3_f32 v227, v227, s6, v1
	v_mul_f32_e32 v228, 0x43800000, v170
	v_mul_f32_e32 v229, 0x43800000, v174
	v_cvt_pk_fp8_f32 v196, v226, v227
	v_med3_f32 v228, v228, s6, v1
	v_med3_f32 v229, v229, s6, v1
	v_cvt_pk_fp8_f32 v196, v228, v229 op_sel:[0,0,1]
	s_waitcnt vmcnt(40)
	v_mul_f32_e32 v226, 0x43800000, v178
	v_mul_f32_e32 v227, 0x43800000, v182
	v_med3_f32 v226, v226, s6, v1
	v_med3_f32 v227, v227, s6, v1
	v_mul_f32_e32 v228, 0x43800000, v186
	v_mul_f32_e32 v229, 0x43800000, v190
	v_cvt_pk_fp8_f32 v197, v226, v227
	v_med3_f32 v228, v228, s6, v1
	v_med3_f32 v229, v229, s6, v1
	v_cvt_pk_fp8_f32 v197, v228, v229 op_sel:[0,0,1]
	s_nop 1
	ds_write_b128 v232, v[194:197] offset:0
	v_mul_f32_e32 v226, 0x43800000, v131
	v_mul_f32_e32 v227, 0x43800000, v135
	v_med3_f32 v226, v226, s6, v1
	v_med3_f32 v227, v227, s6, v1
	v_mul_f32_e32 v228, 0x43800000, v139
	v_mul_f32_e32 v229, 0x43800000, v143
	v_cvt_pk_fp8_f32 v198, v226, v227
	v_med3_f32 v228, v228, s6, v1
	v_med3_f32 v229, v229, s6, v1
	v_cvt_pk_fp8_f32 v198, v228, v229 op_sel:[0,0,1]
	v_mul_f32_e32 v226, 0x43800000, v147
	v_mul_f32_e32 v227, 0x43800000, v151
	v_med3_f32 v226, v226, s6, v1
	v_med3_f32 v227, v227, s6, v1
	v_mul_f32_e32 v228, 0x43800000, v155
	v_mul_f32_e32 v229, 0x43800000, v159
	v_cvt_pk_fp8_f32 v199, v226, v227
	v_med3_f32 v228, v228, s6, v1
	v_med3_f32 v229, v229, s6, v1
	v_cvt_pk_fp8_f32 v199, v228, v229 op_sel:[0,0,1]
	v_mul_f32_e32 v226, 0x43800000, v163
	v_mul_f32_e32 v227, 0x43800000, v167
	v_med3_f32 v226, v226, s6, v1
	v_med3_f32 v227, v227, s6, v1
	v_mul_f32_e32 v228, 0x43800000, v171
	v_mul_f32_e32 v229, 0x43800000, v175
	v_cvt_pk_fp8_f32 v200, v226, v227
	v_med3_f32 v228, v228, s6, v1
	v_med3_f32 v229, v229, s6, v1
	v_cvt_pk_fp8_f32 v200, v228, v229 op_sel:[0,0,1]
	v_mul_f32_e32 v226, 0x43800000, v179
	v_mul_f32_e32 v227, 0x43800000, v183
	v_med3_f32 v226, v226, s6, v1
	v_med3_f32 v227, v227, s6, v1
	v_mul_f32_e32 v228, 0x43800000, v187
	v_mul_f32_e32 v229, 0x43800000, v191
	v_cvt_pk_fp8_f32 v201, v226, v227
	v_med3_f32 v228, v228, s6, v1
	v_med3_f32 v229, v229, s6, v1
	v_cvt_pk_fp8_f32 v201, v228, v229 op_sel:[0,0,1]
	s_nop 1
	ds_write_b128 v232, v[198:201] offset:272
	v_mul_f32_e32 v226, 0x43800000, v132
	v_mul_f32_e32 v227, 0x43800000, v136
	v_med3_f32 v226, v226, s6, v1
	v_med3_f32 v227, v227, s6, v1
	v_mul_f32_e32 v228, 0x43800000, v140
	v_mul_f32_e32 v229, 0x43800000, v144
	v_cvt_pk_fp8_f32 v202, v226, v227
	v_med3_f32 v228, v228, s6, v1
	v_med3_f32 v229, v229, s6, v1
	v_cvt_pk_fp8_f32 v202, v228, v229 op_sel:[0,0,1]
	v_mul_f32_e32 v226, 0x43800000, v148
	v_mul_f32_e32 v227, 0x43800000, v152
	v_med3_f32 v226, v226, s6, v1
	v_med3_f32 v227, v227, s6, v1
	v_mul_f32_e32 v228, 0x43800000, v156
	v_mul_f32_e32 v229, 0x43800000, v160
	v_cvt_pk_fp8_f32 v203, v226, v227
	v_med3_f32 v228, v228, s6, v1
	v_med3_f32 v229, v229, s6, v1
	v_cvt_pk_fp8_f32 v203, v228, v229 op_sel:[0,0,1]
	v_mul_f32_e32 v226, 0x43800000, v164
	v_mul_f32_e32 v227, 0x43800000, v168
	v_med3_f32 v226, v226, s6, v1
	v_med3_f32 v227, v227, s6, v1
	v_mul_f32_e32 v228, 0x43800000, v172
	v_mul_f32_e32 v229, 0x43800000, v176
	v_cvt_pk_fp8_f32 v204, v226, v227
	v_med3_f32 v228, v228, s6, v1
	v_med3_f32 v229, v229, s6, v1
	v_cvt_pk_fp8_f32 v204, v228, v229 op_sel:[0,0,1]
	v_mul_f32_e32 v226, 0x43800000, v180
	v_mul_f32_e32 v227, 0x43800000, v184
	v_med3_f32 v226, v226, s6, v1
	v_med3_f32 v227, v227, s6, v1
	v_mul_f32_e32 v228, 0x43800000, v188
	v_mul_f32_e32 v229, 0x43800000, v192
	v_cvt_pk_fp8_f32 v205, v226, v227
	v_med3_f32 v228, v228, s6, v1
	v_med3_f32 v229, v229, s6, v1
	v_cvt_pk_fp8_f32 v205, v228, v229 op_sel:[0,0,1]
	s_nop 1
	ds_write_b128 v232, v[202:205] offset:544
	v_mul_f32_e32 v226, 0x43800000, v133
	v_mul_f32_e32 v227, 0x43800000, v137
	v_med3_f32 v226, v226, s6, v1
	v_med3_f32 v227, v227, s6, v1
	v_mul_f32_e32 v228, 0x43800000, v141
	v_mul_f32_e32 v229, 0x43800000, v145
	v_cvt_pk_fp8_f32 v206, v226, v227
	v_med3_f32 v228, v228, s6, v1
	v_med3_f32 v229, v229, s6, v1
	v_cvt_pk_fp8_f32 v206, v228, v229 op_sel:[0,0,1]
	v_mul_f32_e32 v226, 0x43800000, v149
	v_mul_f32_e32 v227, 0x43800000, v153
	v_med3_f32 v226, v226, s6, v1
	v_med3_f32 v227, v227, s6, v1
	v_mul_f32_e32 v228, 0x43800000, v157
	v_mul_f32_e32 v229, 0x43800000, v161
	v_cvt_pk_fp8_f32 v207, v226, v227
	v_med3_f32 v228, v228, s6, v1
	v_med3_f32 v229, v229, s6, v1
	v_cvt_pk_fp8_f32 v207, v228, v229 op_sel:[0,0,1]
	v_mul_f32_e32 v226, 0x43800000, v165
	v_mul_f32_e32 v227, 0x43800000, v169
	v_med3_f32 v226, v226, s6, v1
	v_med3_f32 v227, v227, s6, v1
	v_mul_f32_e32 v228, 0x43800000, v173
	v_mul_f32_e32 v229, 0x43800000, v177
	v_cvt_pk_fp8_f32 v208, v226, v227
	v_med3_f32 v228, v228, s6, v1
	v_med3_f32 v229, v229, s6, v1
	v_cvt_pk_fp8_f32 v208, v228, v229 op_sel:[0,0,1]
	v_mul_f32_e32 v226, 0x43800000, v181
	v_mul_f32_e32 v227, 0x43800000, v185
	v_med3_f32 v226, v226, s6, v1
	v_med3_f32 v227, v227, s6, v1
	v_mul_f32_e32 v228, 0x43800000, v189
	v_mul_f32_e32 v229, 0x43800000, v193
	v_cvt_pk_fp8_f32 v209, v226, v227
	v_med3_f32 v228, v228, s6, v1
	v_med3_f32 v229, v229, s6, v1
	v_cvt_pk_fp8_f32 v209, v228, v229 op_sel:[0,0,1]
	s_nop 1
	ds_write_b128 v232, v[206:209] offset:816
	s_waitcnt lgkmcnt(0)
	s_barrier
	global_load_dwordx4 v[130:133], v250, s[0:1] sc0 nt
	global_load_dwordx4 v[134:137], v251, s[0:1] sc0 nt
	global_load_dwordx4 v[138:141], v246, s[0:1] sc0 nt
	global_load_dwordx4 v[142:145], v247, s[0:1] sc0 nt
	global_load_dwordx4 v[146:149], v248, s[0:1] sc0 nt
	global_load_dwordx4 v[150:153], v249, s[0:1] sc0 nt
	global_load_dwordx4 v[154:157], v242, s[0:1] sc0 nt
	global_load_dwordx4 v[158:161], v243, s[0:1] sc0 nt
	global_load_dwordx4 v[162:165], v244, s[0:1] sc0 nt
	global_load_dwordx4 v[166:169], v245, s[0:1] sc0 nt
	global_load_dwordx4 v[170:173], v238, s[0:1] sc0 nt
	global_load_dwordx4 v[174:177], v239, s[0:1] sc0 nt
	global_load_dwordx4 v[178:181], v240, s[0:1] sc0 nt
	global_load_dwordx4 v[182:185], v241, s[0:1] sc0 nt
	global_load_dwordx4 v[186:189], v234, s[0:1] sc0 nt
	global_load_dwordx4 v[190:193], v235, s[0:1] sc0 nt
	s_add_u32 s0, s0, 0x400000
	s_addc_u32 s1, s1, 0
	ds_read_b128 v[194:197], v233 offset:0
	ds_read_b128 v[198:201], v233 offset:8704
	ds_read_b128 v[202:205], v233 offset:17408
	ds_read_b128 v[206:209], v233 offset:26112
	s_waitcnt lgkmcnt(3)
	global_store_dwordx4 v236, v[194:197], s[2:3] nt
	s_waitcnt lgkmcnt(2)
	global_store_dwordx4 v237, v[198:201], s[2:3] nt
	s_waitcnt lgkmcnt(1)
	global_store_dwordx4 v230, v[202:205], s[2:3] nt
	s_waitcnt lgkmcnt(0)
	global_store_dwordx4 v231, v[206:209], s[2:3] nt
	s_add_u32 s2, s2, 0x100
	s_addc_u32 s3, s3, 0
	s_waitcnt vmcnt(56)
	v_mul_f32_e32 v226, 0x43800000, v2
	v_mul_f32_e32 v227, 0x43800000, v6
	v_med3_f32 v226, v226, s6, v1
	v_med3_f32 v227, v227, s6, v1
	v_mul_f32_e32 v228, 0x43800000, v10
	v_mul_f32_e32 v229, 0x43800000, v14
	v_cvt_pk_fp8_f32 v194, v226, v227
	v_med3_f32 v228, v228, s6, v1
	v_med3_f32 v229, v229, s6, v1
	v_cvt_pk_fp8_f32 v194, v228, v229 op_sel:[0,0,1]
	s_waitcnt vmcnt(52)
	v_mul_f32_e32 v226, 0x43800000, v18
	v_mul_f32_e32 v227, 0x43800000, v22
	v_med3_f32 v226, v226, s6, v1
	v_med3_f32 v227, v227, s6, v1
	v_mul_f32_e32 v228, 0x43800000, v26
	v_mul_f32_e32 v229, 0x43800000, v30
	v_cvt_pk_fp8_f32 v195, v226, v227
	v_med3_f32 v228, v228, s6, v1
	v_med3_f32 v229, v229, s6, v1
	v_cvt_pk_fp8_f32 v195, v228, v229 op_sel:[0,0,1]
	s_waitcnt vmcnt(48)
	v_mul_f32_e32 v226, 0x43800000, v34
	v_mul_f32_e32 v227, 0x43800000, v38
	v_med3_f32 v226, v226, s6, v1
	v_med3_f32 v227, v227, s6, v1
	v_mul_f32_e32 v228, 0x43800000, v42
	v_mul_f32_e32 v229, 0x43800000, v46
	v_cvt_pk_fp8_f32 v196, v226, v227
	v_med3_f32 v228, v228, s6, v1
	v_med3_f32 v229, v229, s6, v1
	v_cvt_pk_fp8_f32 v196, v228, v229 op_sel:[0,0,1]
	s_waitcnt vmcnt(44)
	v_mul_f32_e32 v226, 0x43800000, v50
	v_mul_f32_e32 v227, 0x43800000, v54
	v_med3_f32 v226, v226, s6, v1
	v_med3_f32 v227, v227, s6, v1
	v_mul_f32_e32 v228, 0x43800000, v58
	v_mul_f32_e32 v229, 0x43800000, v62
	v_cvt_pk_fp8_f32 v197, v226, v227
	v_med3_f32 v228, v228, s6, v1
	v_med3_f32 v229, v229, s6, v1
	v_cvt_pk_fp8_f32 v197, v228, v229 op_sel:[0,0,1]
	s_nop 1
	ds_write_b128 v232, v[194:197] offset:34816
	v_mul_f32_e32 v226, 0x43800000, v3
	v_mul_f32_e32 v227, 0x43800000, v7
	v_med3_f32 v226, v226, s6, v1
	v_med3_f32 v227, v227, s6, v1
	v_mul_f32_e32 v228, 0x43800000, v11
	v_mul_f32_e32 v229, 0x43800000, v15
	v_cvt_pk_fp8_f32 v198, v226, v227
	v_med3_f32 v228, v228, s6, v1
	v_med3_f32 v229, v229, s6, v1
	v_cvt_pk_fp8_f32 v198, v228, v229 op_sel:[0,0,1]
	v_mul_f32_e32 v226, 0x43800000, v19
	v_mul_f32_e32 v227, 0x43800000, v23
	v_med3_f32 v226, v226, s6, v1
	v_med3_f32 v227, v227, s6, v1
	v_mul_f32_e32 v228, 0x43800000, v27
	v_mul_f32_e32 v229, 0x43800000, v31
	v_cvt_pk_fp8_f32 v199, v226, v227
	v_med3_f32 v228, v228, s6, v1
	v_med3_f32 v229, v229, s6, v1
	v_cvt_pk_fp8_f32 v199, v228, v229 op_sel:[0,0,1]
	v_mul_f32_e32 v226, 0x43800000, v35
	v_mul_f32_e32 v227, 0x43800000, v39
	v_med3_f32 v226, v226, s6, v1
	v_med3_f32 v227, v227, s6, v1
	v_mul_f32_e32 v228, 0x43800000, v43
	v_mul_f32_e32 v229, 0x43800000, v47
	v_cvt_pk_fp8_f32 v200, v226, v227
	v_med3_f32 v228, v228, s6, v1
	v_med3_f32 v229, v229, s6, v1
	v_cvt_pk_fp8_f32 v200, v228, v229 op_sel:[0,0,1]
	v_mul_f32_e32 v226, 0x43800000, v51
	v_mul_f32_e32 v227, 0x43800000, v55
	v_med3_f32 v226, v226, s6, v1
	v_med3_f32 v227, v227, s6, v1
	v_mul_f32_e32 v228, 0x43800000, v59
	v_mul_f32_e32 v229, 0x43800000, v63
	v_cvt_pk_fp8_f32 v201, v226, v227
	v_med3_f32 v228, v228, s6, v1
	v_med3_f32 v229, v229, s6, v1
	v_cvt_pk_fp8_f32 v201, v228, v229 op_sel:[0,0,1]
	s_nop 1
	ds_write_b128 v232, v[198:201] offset:35088
	v_mul_f32_e32 v226, 0x43800000, v4
	v_mul_f32_e32 v227, 0x43800000, v8
	v_med3_f32 v226, v226, s6, v1
	v_med3_f32 v227, v227, s6, v1
	v_mul_f32_e32 v228, 0x43800000, v12
	v_mul_f32_e32 v229, 0x43800000, v16
	v_cvt_pk_fp8_f32 v202, v226, v227
	v_med3_f32 v228, v228, s6, v1
	v_med3_f32 v229, v229, s6, v1
	v_cvt_pk_fp8_f32 v202, v228, v229 op_sel:[0,0,1]
	v_mul_f32_e32 v226, 0x43800000, v20
	v_mul_f32_e32 v227, 0x43800000, v24
	v_med3_f32 v226, v226, s6, v1
	v_med3_f32 v227, v227, s6, v1
	v_mul_f32_e32 v228, 0x43800000, v28
	v_mul_f32_e32 v229, 0x43800000, v32
	v_cvt_pk_fp8_f32 v203, v226, v227
	v_med3_f32 v228, v228, s6, v1
	v_med3_f32 v229, v229, s6, v1
	v_cvt_pk_fp8_f32 v203, v228, v229 op_sel:[0,0,1]
	v_mul_f32_e32 v226, 0x43800000, v36
	v_mul_f32_e32 v227, 0x43800000, v40
	v_med3_f32 v226, v226, s6, v1
	v_med3_f32 v227, v227, s6, v1
	v_mul_f32_e32 v228, 0x43800000, v44
	v_mul_f32_e32 v229, 0x43800000, v48
	v_cvt_pk_fp8_f32 v204, v226, v227
	v_med3_f32 v228, v228, s6, v1
	v_med3_f32 v229, v229, s6, v1
	v_cvt_pk_fp8_f32 v204, v228, v229 op_sel:[0,0,1]
	v_mul_f32_e32 v226, 0x43800000, v52
	v_mul_f32_e32 v227, 0x43800000, v56
	v_med3_f32 v226, v226, s6, v1
	v_med3_f32 v227, v227, s6, v1
	v_mul_f32_e32 v228, 0x43800000, v60
	v_mul_f32_e32 v229, 0x43800000, v64
	v_cvt_pk_fp8_f32 v205, v226, v227
	v_med3_f32 v228, v228, s6, v1
	v_med3_f32 v229, v229, s6, v1
	v_cvt_pk_fp8_f32 v205, v228, v229 op_sel:[0,0,1]
	s_nop 1
	ds_write_b128 v232, v[202:205] offset:35360
	v_mul_f32_e32 v226, 0x43800000, v5
	v_mul_f32_e32 v227, 0x43800000, v9
	v_med3_f32 v226, v226, s6, v1
	v_med3_f32 v227, v227, s6, v1
	v_mul_f32_e32 v228, 0x43800000, v13
	v_mul_f32_e32 v229, 0x43800000, v17
	v_cvt_pk_fp8_f32 v206, v226, v227
	v_med3_f32 v228, v228, s6, v1
	v_med3_f32 v229, v229, s6, v1
	v_cvt_pk_fp8_f32 v206, v228, v229 op_sel:[0,0,1]
	v_mul_f32_e32 v226, 0x43800000, v21
	v_mul_f32_e32 v227, 0x43800000, v25
	v_med3_f32 v226, v226, s6, v1
	v_med3_f32 v227, v227, s6, v1
	v_mul_f32_e32 v228, 0x43800000, v29
	v_mul_f32_e32 v229, 0x43800000, v33
	v_cvt_pk_fp8_f32 v207, v226, v227
	v_med3_f32 v228, v228, s6, v1
	v_med3_f32 v229, v229, s6, v1
	v_cvt_pk_fp8_f32 v207, v228, v229 op_sel:[0,0,1]
	v_mul_f32_e32 v226, 0x43800000, v37
	v_mul_f32_e32 v227, 0x43800000, v41
	v_med3_f32 v226, v226, s6, v1
	v_med3_f32 v227, v227, s6, v1
	v_mul_f32_e32 v228, 0x43800000, v45
	v_mul_f32_e32 v229, 0x43800000, v49
	v_cvt_pk_fp8_f32 v208, v226, v227
	v_med3_f32 v228, v228, s6, v1
	v_med3_f32 v229, v229, s6, v1
	v_cvt_pk_fp8_f32 v208, v228, v229 op_sel:[0,0,1]
	v_mul_f32_e32 v226, 0x43800000, v53
	v_mul_f32_e32 v227, 0x43800000, v57
	v_med3_f32 v226, v226, s6, v1
	v_med3_f32 v227, v227, s6, v1
	v_mul_f32_e32 v228, 0x43800000, v61
	v_mul_f32_e32 v229, 0x43800000, v65
	v_cvt_pk_fp8_f32 v209, v226, v227
	v_med3_f32 v228, v228, s6, v1
	v_med3_f32 v229, v229, s6, v1
	v_cvt_pk_fp8_f32 v209, v228, v229 op_sel:[0,0,1]
	s_nop 1
	ds_write_b128 v232, v[206:209] offset:35632
	s_waitcnt lgkmcnt(0)
	s_barrier
	global_load_dwordx4 v[2:5], v250, s[0:1] sc0 nt
	global_load_dwordx4 v[6:9], v251, s[0:1] sc0 nt
	global_load_dwordx4 v[10:13], v246, s[0:1] sc0 nt
	global_load_dwordx4 v[14:17], v247, s[0:1] sc0 nt
	global_load_dwordx4 v[18:21], v248, s[0:1] sc0 nt
	global_load_dwordx4 v[22:25], v249, s[0:1] sc0 nt
	global_load_dwordx4 v[26:29], v242, s[0:1] sc0 nt
	global_load_dwordx4 v[30:33], v243, s[0:1] sc0 nt
	global_load_dwordx4 v[34:37], v244, s[0:1] sc0 nt
	global_load_dwordx4 v[38:41], v245, s[0:1] sc0 nt
	global_load_dwordx4 v[42:45], v238, s[0:1] sc0 nt
	global_load_dwordx4 v[46:49], v239, s[0:1] sc0 nt
	global_load_dwordx4 v[50:53], v240, s[0:1] sc0 nt
	global_load_dwordx4 v[54:57], v241, s[0:1] sc0 nt
	global_load_dwordx4 v[58:61], v234, s[0:1] sc0 nt
	global_load_dwordx4 v[62:65], v235, s[0:1] sc0 nt
	s_add_u32 s0, s0, 0x400000
	s_addc_u32 s1, s1, 0
	ds_read_b128 v[194:197], v233 offset:34816
	ds_read_b128 v[198:201], v233 offset:43520
	ds_read_b128 v[202:205], v233 offset:52224
	ds_read_b128 v[206:209], v233 offset:60928
	s_waitcnt lgkmcnt(3)
	global_store_dwordx4 v236, v[194:197], s[2:3] nt
	s_waitcnt lgkmcnt(2)
	global_store_dwordx4 v237, v[198:201], s[2:3] nt
	s_waitcnt lgkmcnt(1)
	global_store_dwordx4 v230, v[202:205], s[2:3] nt
	s_waitcnt lgkmcnt(0)
	global_store_dwordx4 v231, v[206:209], s[2:3] nt
	s_add_u32 s2, s2, 0x100
	s_addc_u32 s3, s3, 0
	s_waitcnt vmcnt(56)
	v_mul_f32_e32 v226, 0x43800000, v66
	v_mul_f32_e32 v227, 0x43800000, v70
	v_med3_f32 v226, v226, s6, v1
	v_med3_f32 v227, v227, s6, v1
	v_mul_f32_e32 v228, 0x43800000, v74
	v_mul_f32_e32 v229, 0x43800000, v78
	v_cvt_pk_fp8_f32 v194, v226, v227
	v_med3_f32 v228, v228, s6, v1
	v_med3_f32 v229, v229, s6, v1
	v_cvt_pk_fp8_f32 v194, v228, v229 op_sel:[0,0,1]
	s_waitcnt vmcnt(52)
	v_mul_f32_e32 v226, 0x43800000, v82
	v_mul_f32_e32 v227, 0x43800000, v86
	v_med3_f32 v226, v226, s6, v1
	v_med3_f32 v227, v227, s6, v1
	v_mul_f32_e32 v228, 0x43800000, v90
	v_mul_f32_e32 v229, 0x43800000, v94
	v_cvt_pk_fp8_f32 v195, v226, v227
	v_med3_f32 v228, v228, s6, v1
	v_med3_f32 v229, v229, s6, v1
	v_cvt_pk_fp8_f32 v195, v228, v229 op_sel:[0,0,1]
	s_waitcnt vmcnt(48)
	v_mul_f32_e32 v226, 0x43800000, v98
	v_mul_f32_e32 v227, 0x43800000, v102
	v_med3_f32 v226, v226, s6, v1
	v_med3_f32 v227, v227, s6, v1
	v_mul_f32_e32 v228, 0x43800000, v106
	v_mul_f32_e32 v229, 0x43800000, v110
	v_cvt_pk_fp8_f32 v196, v226, v227
	v_med3_f32 v228, v228, s6, v1
	v_med3_f32 v229, v229, s6, v1
	v_cvt_pk_fp8_f32 v196, v228, v229 op_sel:[0,0,1]
	s_waitcnt vmcnt(44)
	v_mul_f32_e32 v226, 0x43800000, v114
	v_mul_f32_e32 v227, 0x43800000, v118
	v_med3_f32 v226, v226, s6, v1
	v_med3_f32 v227, v227, s6, v1
	v_mul_f32_e32 v228, 0x43800000, v122
	v_mul_f32_e32 v229, 0x43800000, v126
	v_cvt_pk_fp8_f32 v197, v226, v227
	v_med3_f32 v228, v228, s6, v1
	v_med3_f32 v229, v229, s6, v1
	v_cvt_pk_fp8_f32 v197, v228, v229 op_sel:[0,0,1]
	s_nop 1
	ds_write_b128 v232, v[194:197] offset:0
	v_mul_f32_e32 v226, 0x43800000, v67
	v_mul_f32_e32 v227, 0x43800000, v71
	v_med3_f32 v226, v226, s6, v1
	v_med3_f32 v227, v227, s6, v1
	v_mul_f32_e32 v228, 0x43800000, v75
	v_mul_f32_e32 v229, 0x43800000, v79
	v_cvt_pk_fp8_f32 v198, v226, v227
	v_med3_f32 v228, v228, s6, v1
	v_med3_f32 v229, v229, s6, v1
	v_cvt_pk_fp8_f32 v198, v228, v229 op_sel:[0,0,1]
	v_mul_f32_e32 v226, 0x43800000, v83
	v_mul_f32_e32 v227, 0x43800000, v87
	v_med3_f32 v226, v226, s6, v1
	v_med3_f32 v227, v227, s6, v1
	v_mul_f32_e32 v228, 0x43800000, v91
	v_mul_f32_e32 v229, 0x43800000, v95
	v_cvt_pk_fp8_f32 v199, v226, v227
	v_med3_f32 v228, v228, s6, v1
	v_med3_f32 v229, v229, s6, v1
	v_cvt_pk_fp8_f32 v199, v228, v229 op_sel:[0,0,1]
	v_mul_f32_e32 v226, 0x43800000, v99
	v_mul_f32_e32 v227, 0x43800000, v103
	v_med3_f32 v226, v226, s6, v1
	v_med3_f32 v227, v227, s6, v1
	v_mul_f32_e32 v228, 0x43800000, v107
	v_mul_f32_e32 v229, 0x43800000, v111
	v_cvt_pk_fp8_f32 v200, v226, v227
	v_med3_f32 v228, v228, s6, v1
	v_med3_f32 v229, v229, s6, v1
	v_cvt_pk_fp8_f32 v200, v228, v229 op_sel:[0,0,1]
	v_mul_f32_e32 v226, 0x43800000, v115
	v_mul_f32_e32 v227, 0x43800000, v119
	v_med3_f32 v226, v226, s6, v1
	v_med3_f32 v227, v227, s6, v1
	v_mul_f32_e32 v228, 0x43800000, v123
	v_mul_f32_e32 v229, 0x43800000, v127
	v_cvt_pk_fp8_f32 v201, v226, v227
	v_med3_f32 v228, v228, s6, v1
	v_med3_f32 v229, v229, s6, v1
	v_cvt_pk_fp8_f32 v201, v228, v229 op_sel:[0,0,1]
	s_nop 1
	ds_write_b128 v232, v[198:201] offset:272
	v_mul_f32_e32 v226, 0x43800000, v68
	v_mul_f32_e32 v227, 0x43800000, v72
	v_med3_f32 v226, v226, s6, v1
	v_med3_f32 v227, v227, s6, v1
	v_mul_f32_e32 v228, 0x43800000, v76
	v_mul_f32_e32 v229, 0x43800000, v80
	v_cvt_pk_fp8_f32 v202, v226, v227
	v_med3_f32 v228, v228, s6, v1
	v_med3_f32 v229, v229, s6, v1
	v_cvt_pk_fp8_f32 v202, v228, v229 op_sel:[0,0,1]
	v_mul_f32_e32 v226, 0x43800000, v84
	v_mul_f32_e32 v227, 0x43800000, v88
	v_med3_f32 v226, v226, s6, v1
	v_med3_f32 v227, v227, s6, v1
	v_mul_f32_e32 v228, 0x43800000, v92
	v_mul_f32_e32 v229, 0x43800000, v96
	v_cvt_pk_fp8_f32 v203, v226, v227
	v_med3_f32 v228, v228, s6, v1
	v_med3_f32 v229, v229, s6, v1
	v_cvt_pk_fp8_f32 v203, v228, v229 op_sel:[0,0,1]
	v_mul_f32_e32 v226, 0x43800000, v100
	v_mul_f32_e32 v227, 0x43800000, v104
	v_med3_f32 v226, v226, s6, v1
	v_med3_f32 v227, v227, s6, v1
	v_mul_f32_e32 v228, 0x43800000, v108
	v_mul_f32_e32 v229, 0x43800000, v112
	v_cvt_pk_fp8_f32 v204, v226, v227
	v_med3_f32 v228, v228, s6, v1
	v_med3_f32 v229, v229, s6, v1
	v_cvt_pk_fp8_f32 v204, v228, v229 op_sel:[0,0,1]
	v_mul_f32_e32 v226, 0x43800000, v116
	v_mul_f32_e32 v227, 0x43800000, v120
	v_med3_f32 v226, v226, s6, v1
	v_med3_f32 v227, v227, s6, v1
	v_mul_f32_e32 v228, 0x43800000, v124
	v_mul_f32_e32 v229, 0x43800000, v128
	v_cvt_pk_fp8_f32 v205, v226, v227
	v_med3_f32 v228, v228, s6, v1
	v_med3_f32 v229, v229, s6, v1
	v_cvt_pk_fp8_f32 v205, v228, v229 op_sel:[0,0,1]
	s_nop 1
	ds_write_b128 v232, v[202:205] offset:544
	v_mul_f32_e32 v226, 0x43800000, v69
	v_mul_f32_e32 v227, 0x43800000, v73
	v_med3_f32 v226, v226, s6, v1
	v_med3_f32 v227, v227, s6, v1
	v_mul_f32_e32 v228, 0x43800000, v77
	v_mul_f32_e32 v229, 0x43800000, v81
	v_cvt_pk_fp8_f32 v206, v226, v227
	v_med3_f32 v228, v228, s6, v1
	v_med3_f32 v229, v229, s6, v1
	v_cvt_pk_fp8_f32 v206, v228, v229 op_sel:[0,0,1]
	v_mul_f32_e32 v226, 0x43800000, v85
	v_mul_f32_e32 v227, 0x43800000, v89
	v_med3_f32 v226, v226, s6, v1
	v_med3_f32 v227, v227, s6, v1
	v_mul_f32_e32 v228, 0x43800000, v93
	v_mul_f32_e32 v229, 0x43800000, v97
	v_cvt_pk_fp8_f32 v207, v226, v227
	v_med3_f32 v228, v228, s6, v1
	v_med3_f32 v229, v229, s6, v1
	v_cvt_pk_fp8_f32 v207, v228, v229 op_sel:[0,0,1]
	v_mul_f32_e32 v226, 0x43800000, v101
	v_mul_f32_e32 v227, 0x43800000, v105
	v_med3_f32 v226, v226, s6, v1
	v_med3_f32 v227, v227, s6, v1
	v_mul_f32_e32 v228, 0x43800000, v109
	v_mul_f32_e32 v229, 0x43800000, v113
	v_cvt_pk_fp8_f32 v208, v226, v227
	v_med3_f32 v228, v228, s6, v1
	v_med3_f32 v229, v229, s6, v1
	v_cvt_pk_fp8_f32 v208, v228, v229 op_sel:[0,0,1]
	v_mul_f32_e32 v226, 0x43800000, v117
	v_mul_f32_e32 v227, 0x43800000, v121
	v_med3_f32 v226, v226, s6, v1
	v_med3_f32 v227, v227, s6, v1
	v_mul_f32_e32 v228, 0x43800000, v125
	v_mul_f32_e32 v229, 0x43800000, v129
	v_cvt_pk_fp8_f32 v209, v226, v227
	v_med3_f32 v228, v228, s6, v1
	v_med3_f32 v229, v229, s6, v1
	v_cvt_pk_fp8_f32 v209, v228, v229 op_sel:[0,0,1]
	s_nop 1
	ds_write_b128 v232, v[206:209] offset:816
	s_waitcnt lgkmcnt(0)
	s_barrier
	global_load_dwordx4 v[66:69], v250, s[0:1] sc0 nt
	global_load_dwordx4 v[70:73], v251, s[0:1] sc0 nt
	global_load_dwordx4 v[74:77], v246, s[0:1] sc0 nt
	global_load_dwordx4 v[78:81], v247, s[0:1] sc0 nt
	global_load_dwordx4 v[82:85], v248, s[0:1] sc0 nt
	global_load_dwordx4 v[86:89], v249, s[0:1] sc0 nt
	global_load_dwordx4 v[90:93], v242, s[0:1] sc0 nt
	global_load_dwordx4 v[94:97], v243, s[0:1] sc0 nt
	global_load_dwordx4 v[98:101], v244, s[0:1] sc0 nt
	global_load_dwordx4 v[102:105], v245, s[0:1] sc0 nt
	global_load_dwordx4 v[106:109], v238, s[0:1] sc0 nt
	global_load_dwordx4 v[110:113], v239, s[0:1] sc0 nt
	global_load_dwordx4 v[114:117], v240, s[0:1] sc0 nt
	global_load_dwordx4 v[118:121], v241, s[0:1] sc0 nt
	global_load_dwordx4 v[122:125], v234, s[0:1] sc0 nt
	global_load_dwordx4 v[126:129], v235, s[0:1] sc0 nt
	s_add_u32 s0, s0, 0x400000
	s_addc_u32 s1, s1, 0
	ds_read_b128 v[194:197], v233 offset:0
	ds_read_b128 v[198:201], v233 offset:8704
	ds_read_b128 v[202:205], v233 offset:17408
	ds_read_b128 v[206:209], v233 offset:26112
	s_waitcnt lgkmcnt(3)
	global_store_dwordx4 v236, v[194:197], s[2:3] nt
	s_waitcnt lgkmcnt(2)
	global_store_dwordx4 v237, v[198:201], s[2:3] nt
	s_waitcnt lgkmcnt(1)
	global_store_dwordx4 v230, v[202:205], s[2:3] nt
	s_waitcnt lgkmcnt(0)
	global_store_dwordx4 v231, v[206:209], s[2:3] nt
	s_add_u32 s2, s2, 0x100
	s_addc_u32 s3, s3, 0
	s_waitcnt vmcnt(56)
	v_mul_f32_e32 v226, 0x43800000, v130
	v_mul_f32_e32 v227, 0x43800000, v134
	v_med3_f32 v226, v226, s6, v1
	v_med3_f32 v227, v227, s6, v1
	v_mul_f32_e32 v228, 0x43800000, v138
	v_mul_f32_e32 v229, 0x43800000, v142
	v_cvt_pk_fp8_f32 v194, v226, v227
	v_med3_f32 v228, v228, s6, v1
	v_med3_f32 v229, v229, s6, v1
	v_cvt_pk_fp8_f32 v194, v228, v229 op_sel:[0,0,1]
	s_waitcnt vmcnt(52)
	v_mul_f32_e32 v226, 0x43800000, v146
	v_mul_f32_e32 v227, 0x43800000, v150
	v_med3_f32 v226, v226, s6, v1
	v_med3_f32 v227, v227, s6, v1
	v_mul_f32_e32 v228, 0x43800000, v154
	v_mul_f32_e32 v229, 0x43800000, v158
	v_cvt_pk_fp8_f32 v195, v226, v227
	v_med3_f32 v228, v228, s6, v1
	v_med3_f32 v229, v229, s6, v1
	v_cvt_pk_fp8_f32 v195, v228, v229 op_sel:[0,0,1]
	s_waitcnt vmcnt(48)
	v_mul_f32_e32 v226, 0x43800000, v162
	v_mul_f32_e32 v227, 0x43800000, v166
	v_med3_f32 v226, v226, s6, v1
	v_med3_f32 v227, v227, s6, v1
	v_mul_f32_e32 v228, 0x43800000, v170
	v_mul_f32_e32 v229, 0x43800000, v174
	v_cvt_pk_fp8_f32 v196, v226, v227
	v_med3_f32 v228, v228, s6, v1
	v_med3_f32 v229, v229, s6, v1
	v_cvt_pk_fp8_f32 v196, v228, v229 op_sel:[0,0,1]
	s_waitcnt vmcnt(44)
	v_mul_f32_e32 v226, 0x43800000, v178
	v_mul_f32_e32 v227, 0x43800000, v182
	v_med3_f32 v226, v226, s6, v1
	v_med3_f32 v227, v227, s6, v1
	v_mul_f32_e32 v228, 0x43800000, v186
	v_mul_f32_e32 v229, 0x43800000, v190
	v_cvt_pk_fp8_f32 v197, v226, v227
	v_med3_f32 v228, v228, s6, v1
	v_med3_f32 v229, v229, s6, v1
	v_cvt_pk_fp8_f32 v197, v228, v229 op_sel:[0,0,1]
	s_nop 1
	ds_write_b128 v232, v[194:197] offset:34816
	v_mul_f32_e32 v226, 0x43800000, v131
	v_mul_f32_e32 v227, 0x43800000, v135
	v_med3_f32 v226, v226, s6, v1
	v_med3_f32 v227, v227, s6, v1
	v_mul_f32_e32 v228, 0x43800000, v139
	v_mul_f32_e32 v229, 0x43800000, v143
	v_cvt_pk_fp8_f32 v198, v226, v227
	v_med3_f32 v228, v228, s6, v1
	v_med3_f32 v229, v229, s6, v1
	v_cvt_pk_fp8_f32 v198, v228, v229 op_sel:[0,0,1]
	v_mul_f32_e32 v226, 0x43800000, v147
	v_mul_f32_e32 v227, 0x43800000, v151
	v_med3_f32 v226, v226, s6, v1
	v_med3_f32 v227, v227, s6, v1
	v_mul_f32_e32 v228, 0x43800000, v155
	v_mul_f32_e32 v229, 0x43800000, v159
	v_cvt_pk_fp8_f32 v199, v226, v227
	v_med3_f32 v228, v228, s6, v1
	v_med3_f32 v229, v229, s6, v1
	v_cvt_pk_fp8_f32 v199, v228, v229 op_sel:[0,0,1]
	v_mul_f32_e32 v226, 0x43800000, v163
	v_mul_f32_e32 v227, 0x43800000, v167
	v_med3_f32 v226, v226, s6, v1
	v_med3_f32 v227, v227, s6, v1
	v_mul_f32_e32 v228, 0x43800000, v171
	v_mul_f32_e32 v229, 0x43800000, v175
	v_cvt_pk_fp8_f32 v200, v226, v227
	v_med3_f32 v228, v228, s6, v1
	v_med3_f32 v229, v229, s6, v1
	v_cvt_pk_fp8_f32 v200, v228, v229 op_sel:[0,0,1]
	v_mul_f32_e32 v226, 0x43800000, v179
	v_mul_f32_e32 v227, 0x43800000, v183
	v_med3_f32 v226, v226, s6, v1
	v_med3_f32 v227, v227, s6, v1
	v_mul_f32_e32 v228, 0x43800000, v187
	v_mul_f32_e32 v229, 0x43800000, v191
	v_cvt_pk_fp8_f32 v201, v226, v227
	v_med3_f32 v228, v228, s6, v1
	v_med3_f32 v229, v229, s6, v1
	v_cvt_pk_fp8_f32 v201, v228, v229 op_sel:[0,0,1]
	s_nop 1
	ds_write_b128 v232, v[198:201] offset:35088
	v_mul_f32_e32 v226, 0x43800000, v132
	v_mul_f32_e32 v227, 0x43800000, v136
	v_med3_f32 v226, v226, s6, v1
	v_med3_f32 v227, v227, s6, v1
	v_mul_f32_e32 v228, 0x43800000, v140
	v_mul_f32_e32 v229, 0x43800000, v144
	v_cvt_pk_fp8_f32 v202, v226, v227
	v_med3_f32 v228, v228, s6, v1
	v_med3_f32 v229, v229, s6, v1
	v_cvt_pk_fp8_f32 v202, v228, v229 op_sel:[0,0,1]
	v_mul_f32_e32 v226, 0x43800000, v148
	v_mul_f32_e32 v227, 0x43800000, v152
	v_med3_f32 v226, v226, s6, v1
	v_med3_f32 v227, v227, s6, v1
	v_mul_f32_e32 v228, 0x43800000, v156
	v_mul_f32_e32 v229, 0x43800000, v160
	v_cvt_pk_fp8_f32 v203, v226, v227
	v_med3_f32 v228, v228, s6, v1
	v_med3_f32 v229, v229, s6, v1
	v_cvt_pk_fp8_f32 v203, v228, v229 op_sel:[0,0,1]
	v_mul_f32_e32 v226, 0x43800000, v164
	v_mul_f32_e32 v227, 0x43800000, v168
	v_med3_f32 v226, v226, s6, v1
	v_med3_f32 v227, v227, s6, v1
	v_mul_f32_e32 v228, 0x43800000, v172
	v_mul_f32_e32 v229, 0x43800000, v176
	v_cvt_pk_fp8_f32 v204, v226, v227
	v_med3_f32 v228, v228, s6, v1
	v_med3_f32 v229, v229, s6, v1
	v_cvt_pk_fp8_f32 v204, v228, v229 op_sel:[0,0,1]
	v_mul_f32_e32 v226, 0x43800000, v180
	v_mul_f32_e32 v227, 0x43800000, v184
	v_med3_f32 v226, v226, s6, v1
	v_med3_f32 v227, v227, s6, v1
	v_mul_f32_e32 v228, 0x43800000, v188
	v_mul_f32_e32 v229, 0x43800000, v192
	v_cvt_pk_fp8_f32 v205, v226, v227
	v_med3_f32 v228, v228, s6, v1
	v_med3_f32 v229, v229, s6, v1
	v_cvt_pk_fp8_f32 v205, v228, v229 op_sel:[0,0,1]
	s_nop 1
	ds_write_b128 v232, v[202:205] offset:35360
	v_mul_f32_e32 v226, 0x43800000, v133
	v_mul_f32_e32 v227, 0x43800000, v137
	v_med3_f32 v226, v226, s6, v1
	v_med3_f32 v227, v227, s6, v1
	v_mul_f32_e32 v228, 0x43800000, v141
	v_mul_f32_e32 v229, 0x43800000, v145
	v_cvt_pk_fp8_f32 v206, v226, v227
	v_med3_f32 v228, v228, s6, v1
	v_med3_f32 v229, v229, s6, v1
	v_cvt_pk_fp8_f32 v206, v228, v229 op_sel:[0,0,1]
	v_mul_f32_e32 v226, 0x43800000, v149
	v_mul_f32_e32 v227, 0x43800000, v153
	v_med3_f32 v226, v226, s6, v1
	v_med3_f32 v227, v227, s6, v1
	v_mul_f32_e32 v228, 0x43800000, v157
	v_mul_f32_e32 v229, 0x43800000, v161
	v_cvt_pk_fp8_f32 v207, v226, v227
	v_med3_f32 v228, v228, s6, v1
	v_med3_f32 v229, v229, s6, v1
	v_cvt_pk_fp8_f32 v207, v228, v229 op_sel:[0,0,1]
	v_mul_f32_e32 v226, 0x43800000, v165
	v_mul_f32_e32 v227, 0x43800000, v169
	v_med3_f32 v226, v226, s6, v1
	v_med3_f32 v227, v227, s6, v1
	v_mul_f32_e32 v228, 0x43800000, v173
	v_mul_f32_e32 v229, 0x43800000, v177
	v_cvt_pk_fp8_f32 v208, v226, v227
	v_med3_f32 v228, v228, s6, v1
	v_med3_f32 v229, v229, s6, v1
	v_cvt_pk_fp8_f32 v208, v228, v229 op_sel:[0,0,1]
	v_mul_f32_e32 v226, 0x43800000, v181
	v_mul_f32_e32 v227, 0x43800000, v185
	v_med3_f32 v226, v226, s6, v1
	v_med3_f32 v227, v227, s6, v1
	v_mul_f32_e32 v228, 0x43800000, v189
	v_mul_f32_e32 v229, 0x43800000, v193
	v_cvt_pk_fp8_f32 v209, v226, v227
	v_med3_f32 v228, v228, s6, v1
	v_med3_f32 v229, v229, s6, v1
	v_cvt_pk_fp8_f32 v209, v228, v229 op_sel:[0,0,1]
	s_nop 1
	ds_write_b128 v232, v[206:209] offset:35632
	s_waitcnt lgkmcnt(0)
	s_barrier
	ds_read_b128 v[194:197], v233 offset:34816
	ds_read_b128 v[198:201], v233 offset:43520
	ds_read_b128 v[202:205], v233 offset:52224
	ds_read_b128 v[206:209], v233 offset:60928
	s_waitcnt lgkmcnt(3)
	global_store_dwordx4 v236, v[194:197], s[2:3] nt
	s_waitcnt lgkmcnt(2)
	global_store_dwordx4 v237, v[198:201], s[2:3] nt
	s_waitcnt lgkmcnt(1)
	global_store_dwordx4 v230, v[202:205], s[2:3] nt
	s_waitcnt lgkmcnt(0)
	global_store_dwordx4 v231, v[206:209], s[2:3] nt
	s_add_u32 s2, s2, 0x100
	s_addc_u32 s3, s3, 0
	s_waitcnt vmcnt(40)
	v_mul_f32_e32 v226, 0x43800000, v2
	v_mul_f32_e32 v227, 0x43800000, v6
	v_med3_f32 v226, v226, s6, v1
	v_med3_f32 v227, v227, s6, v1
	v_mul_f32_e32 v228, 0x43800000, v10
	v_mul_f32_e32 v229, 0x43800000, v14
	v_cvt_pk_fp8_f32 v194, v226, v227
	v_med3_f32 v228, v228, s6, v1
	v_med3_f32 v229, v229, s6, v1
	v_cvt_pk_fp8_f32 v194, v228, v229 op_sel:[0,0,1]
	s_waitcnt vmcnt(36)
	v_mul_f32_e32 v226, 0x43800000, v18
	v_mul_f32_e32 v227, 0x43800000, v22
	v_med3_f32 v226, v226, s6, v1
	v_med3_f32 v227, v227, s6, v1
	v_mul_f32_e32 v228, 0x43800000, v26
	v_mul_f32_e32 v229, 0x43800000, v30
	v_cvt_pk_fp8_f32 v195, v226, v227
	v_med3_f32 v228, v228, s6, v1
	v_med3_f32 v229, v229, s6, v1
	v_cvt_pk_fp8_f32 v195, v228, v229 op_sel:[0,0,1]
	s_waitcnt vmcnt(32)
	v_mul_f32_e32 v226, 0x43800000, v34
	v_mul_f32_e32 v227, 0x43800000, v38
	v_med3_f32 v226, v226, s6, v1
	v_med3_f32 v227, v227, s6, v1
	v_mul_f32_e32 v228, 0x43800000, v42
	v_mul_f32_e32 v229, 0x43800000, v46
	v_cvt_pk_fp8_f32 v196, v226, v227
	v_med3_f32 v228, v228, s6, v1
	v_med3_f32 v229, v229, s6, v1
	v_cvt_pk_fp8_f32 v196, v228, v229 op_sel:[0,0,1]
	s_waitcnt vmcnt(28)
	v_mul_f32_e32 v226, 0x43800000, v50
	v_mul_f32_e32 v227, 0x43800000, v54
	v_med3_f32 v226, v226, s6, v1
	v_med3_f32 v227, v227, s6, v1
	v_mul_f32_e32 v228, 0x43800000, v58
	v_mul_f32_e32 v229, 0x43800000, v62
	v_cvt_pk_fp8_f32 v197, v226, v227
	v_med3_f32 v228, v228, s6, v1
	v_med3_f32 v229, v229, s6, v1
	v_cvt_pk_fp8_f32 v197, v228, v229 op_sel:[0,0,1]
	s_nop 1
	ds_write_b128 v232, v[194:197] offset:0
	v_mul_f32_e32 v226, 0x43800000, v3
	v_mul_f32_e32 v227, 0x43800000, v7
	v_med3_f32 v226, v226, s6, v1
	v_med3_f32 v227, v227, s6, v1
	v_mul_f32_e32 v228, 0x43800000, v11
	v_mul_f32_e32 v229, 0x43800000, v15
	v_cvt_pk_fp8_f32 v198, v226, v227
	v_med3_f32 v228, v228, s6, v1
	v_med3_f32 v229, v229, s6, v1
	v_cvt_pk_fp8_f32 v198, v228, v229 op_sel:[0,0,1]
	v_mul_f32_e32 v226, 0x43800000, v19
	v_mul_f32_e32 v227, 0x43800000, v23
	v_med3_f32 v226, v226, s6, v1
	v_med3_f32 v227, v227, s6, v1
	v_mul_f32_e32 v228, 0x43800000, v27
	v_mul_f32_e32 v229, 0x43800000, v31
	v_cvt_pk_fp8_f32 v199, v226, v227
	v_med3_f32 v228, v228, s6, v1
	v_med3_f32 v229, v229, s6, v1
	v_cvt_pk_fp8_f32 v199, v228, v229 op_sel:[0,0,1]
	v_mul_f32_e32 v226, 0x43800000, v35
	v_mul_f32_e32 v227, 0x43800000, v39
	v_med3_f32 v226, v226, s6, v1
	v_med3_f32 v227, v227, s6, v1
	v_mul_f32_e32 v228, 0x43800000, v43
	v_mul_f32_e32 v229, 0x43800000, v47
	v_cvt_pk_fp8_f32 v200, v226, v227
	v_med3_f32 v228, v228, s6, v1
	v_med3_f32 v229, v229, s6, v1
	v_cvt_pk_fp8_f32 v200, v228, v229 op_sel:[0,0,1]
	v_mul_f32_e32 v226, 0x43800000, v51
	v_mul_f32_e32 v227, 0x43800000, v55
	v_med3_f32 v226, v226, s6, v1
	v_med3_f32 v227, v227, s6, v1
	v_mul_f32_e32 v228, 0x43800000, v59
	v_mul_f32_e32 v229, 0x43800000, v63
	v_cvt_pk_fp8_f32 v201, v226, v227
	v_med3_f32 v228, v228, s6, v1
	v_med3_f32 v229, v229, s6, v1
	v_cvt_pk_fp8_f32 v201, v228, v229 op_sel:[0,0,1]
	s_nop 1
	ds_write_b128 v232, v[198:201] offset:272
	v_mul_f32_e32 v226, 0x43800000, v4
	v_mul_f32_e32 v227, 0x43800000, v8
	v_med3_f32 v226, v226, s6, v1
	v_med3_f32 v227, v227, s6, v1
	v_mul_f32_e32 v228, 0x43800000, v12
	v_mul_f32_e32 v229, 0x43800000, v16
	v_cvt_pk_fp8_f32 v202, v226, v227
	v_med3_f32 v228, v228, s6, v1
	v_med3_f32 v229, v229, s6, v1
	v_cvt_pk_fp8_f32 v202, v228, v229 op_sel:[0,0,1]
	v_mul_f32_e32 v226, 0x43800000, v20
	v_mul_f32_e32 v227, 0x43800000, v24
	v_med3_f32 v226, v226, s6, v1
	v_med3_f32 v227, v227, s6, v1
	v_mul_f32_e32 v228, 0x43800000, v28
	v_mul_f32_e32 v229, 0x43800000, v32
	v_cvt_pk_fp8_f32 v203, v226, v227
	v_med3_f32 v228, v228, s6, v1
	v_med3_f32 v229, v229, s6, v1
	v_cvt_pk_fp8_f32 v203, v228, v229 op_sel:[0,0,1]
	v_mul_f32_e32 v226, 0x43800000, v36
	v_mul_f32_e32 v227, 0x43800000, v40
	v_med3_f32 v226, v226, s6, v1
	v_med3_f32 v227, v227, s6, v1
	v_mul_f32_e32 v228, 0x43800000, v44
	v_mul_f32_e32 v229, 0x43800000, v48
	v_cvt_pk_fp8_f32 v204, v226, v227
	v_med3_f32 v228, v228, s6, v1
	v_med3_f32 v229, v229, s6, v1
	v_cvt_pk_fp8_f32 v204, v228, v229 op_sel:[0,0,1]
	v_mul_f32_e32 v226, 0x43800000, v52
	v_mul_f32_e32 v227, 0x43800000, v56
	v_med3_f32 v226, v226, s6, v1
	v_med3_f32 v227, v227, s6, v1
	v_mul_f32_e32 v228, 0x43800000, v60
	v_mul_f32_e32 v229, 0x43800000, v64
	v_cvt_pk_fp8_f32 v205, v226, v227
	v_med3_f32 v228, v228, s6, v1
	v_med3_f32 v229, v229, s6, v1
	v_cvt_pk_fp8_f32 v205, v228, v229 op_sel:[0,0,1]
	s_nop 1
	ds_write_b128 v232, v[202:205] offset:544
	v_mul_f32_e32 v226, 0x43800000, v5
	v_mul_f32_e32 v227, 0x43800000, v9
	v_med3_f32 v226, v226, s6, v1
	v_med3_f32 v227, v227, s6, v1
	v_mul_f32_e32 v228, 0x43800000, v13
	v_mul_f32_e32 v229, 0x43800000, v17
	v_cvt_pk_fp8_f32 v206, v226, v227
	v_med3_f32 v228, v228, s6, v1
	v_med3_f32 v229, v229, s6, v1
	v_cvt_pk_fp8_f32 v206, v228, v229 op_sel:[0,0,1]
	v_mul_f32_e32 v226, 0x43800000, v21
	v_mul_f32_e32 v227, 0x43800000, v25
	v_med3_f32 v226, v226, s6, v1
	v_med3_f32 v227, v227, s6, v1
	v_mul_f32_e32 v228, 0x43800000, v29
	v_mul_f32_e32 v229, 0x43800000, v33
	v_cvt_pk_fp8_f32 v207, v226, v227
	v_med3_f32 v228, v228, s6, v1
	v_med3_f32 v229, v229, s6, v1
	v_cvt_pk_fp8_f32 v207, v228, v229 op_sel:[0,0,1]
	v_mul_f32_e32 v226, 0x43800000, v37
	v_mul_f32_e32 v227, 0x43800000, v41
	v_med3_f32 v226, v226, s6, v1
	v_med3_f32 v227, v227, s6, v1
	v_mul_f32_e32 v228, 0x43800000, v45
	v_mul_f32_e32 v229, 0x43800000, v49
	v_cvt_pk_fp8_f32 v208, v226, v227
	v_med3_f32 v228, v228, s6, v1
	v_med3_f32 v229, v229, s6, v1
	v_cvt_pk_fp8_f32 v208, v228, v229 op_sel:[0,0,1]
	v_mul_f32_e32 v226, 0x43800000, v53
	v_mul_f32_e32 v227, 0x43800000, v57
	v_med3_f32 v226, v226, s6, v1
	v_med3_f32 v227, v227, s6, v1
	v_mul_f32_e32 v228, 0x43800000, v61
	v_mul_f32_e32 v229, 0x43800000, v65
	v_cvt_pk_fp8_f32 v209, v226, v227
	v_med3_f32 v228, v228, s6, v1
	v_med3_f32 v229, v229, s6, v1
	v_cvt_pk_fp8_f32 v209, v228, v229 op_sel:[0,0,1]
	s_nop 1
	ds_write_b128 v232, v[206:209] offset:816
	s_waitcnt lgkmcnt(0)
	s_barrier
	ds_read_b128 v[194:197], v233 offset:0
	ds_read_b128 v[198:201], v233 offset:8704
	ds_read_b128 v[202:205], v233 offset:17408
	ds_read_b128 v[206:209], v233 offset:26112
	s_waitcnt lgkmcnt(3)
	global_store_dwordx4 v236, v[194:197], s[2:3] nt
	s_waitcnt lgkmcnt(2)
	global_store_dwordx4 v237, v[198:201], s[2:3] nt
	s_waitcnt lgkmcnt(1)
	global_store_dwordx4 v230, v[202:205], s[2:3] nt
	s_waitcnt lgkmcnt(0)
	global_store_dwordx4 v231, v[206:209], s[2:3] nt
	s_add_u32 s2, s2, 0x100
	s_addc_u32 s3, s3, 0
	s_waitcnt vmcnt(24)
	v_mul_f32_e32 v226, 0x43800000, v66
	v_mul_f32_e32 v227, 0x43800000, v70
	v_med3_f32 v226, v226, s6, v1
	v_med3_f32 v227, v227, s6, v1
	v_mul_f32_e32 v228, 0x43800000, v74
	v_mul_f32_e32 v229, 0x43800000, v78
	v_cvt_pk_fp8_f32 v194, v226, v227
	v_med3_f32 v228, v228, s6, v1
	v_med3_f32 v229, v229, s6, v1
	v_cvt_pk_fp8_f32 v194, v228, v229 op_sel:[0,0,1]
	s_waitcnt vmcnt(20)
	v_mul_f32_e32 v226, 0x43800000, v82
	v_mul_f32_e32 v227, 0x43800000, v86
	v_med3_f32 v226, v226, s6, v1
	v_med3_f32 v227, v227, s6, v1
	v_mul_f32_e32 v228, 0x43800000, v90
	v_mul_f32_e32 v229, 0x43800000, v94
	v_cvt_pk_fp8_f32 v195, v226, v227
	v_med3_f32 v228, v228, s6, v1
	v_med3_f32 v229, v229, s6, v1
	v_cvt_pk_fp8_f32 v195, v228, v229 op_sel:[0,0,1]
	s_waitcnt vmcnt(16)
	v_mul_f32_e32 v226, 0x43800000, v98
	v_mul_f32_e32 v227, 0x43800000, v102
	v_med3_f32 v226, v226, s6, v1
	v_med3_f32 v227, v227, s6, v1
	v_mul_f32_e32 v228, 0x43800000, v106
	v_mul_f32_e32 v229, 0x43800000, v110
	v_cvt_pk_fp8_f32 v196, v226, v227
	v_med3_f32 v228, v228, s6, v1
	v_med3_f32 v229, v229, s6, v1
	v_cvt_pk_fp8_f32 v196, v228, v229 op_sel:[0,0,1]
	s_waitcnt vmcnt(12)
	v_mul_f32_e32 v226, 0x43800000, v114
	v_mul_f32_e32 v227, 0x43800000, v118
	v_med3_f32 v226, v226, s6, v1
	v_med3_f32 v227, v227, s6, v1
	v_mul_f32_e32 v228, 0x43800000, v122
	v_mul_f32_e32 v229, 0x43800000, v126
	v_cvt_pk_fp8_f32 v197, v226, v227
	v_med3_f32 v228, v228, s6, v1
	v_med3_f32 v229, v229, s6, v1
	v_cvt_pk_fp8_f32 v197, v228, v229 op_sel:[0,0,1]
	s_nop 1
	ds_write_b128 v232, v[194:197] offset:34816
	v_mul_f32_e32 v226, 0x43800000, v67
	v_mul_f32_e32 v227, 0x43800000, v71
	v_med3_f32 v226, v226, s6, v1
	v_med3_f32 v227, v227, s6, v1
	v_mul_f32_e32 v228, 0x43800000, v75
	v_mul_f32_e32 v229, 0x43800000, v79
	v_cvt_pk_fp8_f32 v198, v226, v227
	v_med3_f32 v228, v228, s6, v1
	v_med3_f32 v229, v229, s6, v1
	v_cvt_pk_fp8_f32 v198, v228, v229 op_sel:[0,0,1]
	v_mul_f32_e32 v226, 0x43800000, v83
	v_mul_f32_e32 v227, 0x43800000, v87
	v_med3_f32 v226, v226, s6, v1
	v_med3_f32 v227, v227, s6, v1
	v_mul_f32_e32 v228, 0x43800000, v91
	v_mul_f32_e32 v229, 0x43800000, v95
	v_cvt_pk_fp8_f32 v199, v226, v227
	v_med3_f32 v228, v228, s6, v1
	v_med3_f32 v229, v229, s6, v1
	v_cvt_pk_fp8_f32 v199, v228, v229 op_sel:[0,0,1]
	v_mul_f32_e32 v226, 0x43800000, v99
	v_mul_f32_e32 v227, 0x43800000, v103
	v_med3_f32 v226, v226, s6, v1
	v_med3_f32 v227, v227, s6, v1
	v_mul_f32_e32 v228, 0x43800000, v107
	v_mul_f32_e32 v229, 0x43800000, v111
	v_cvt_pk_fp8_f32 v200, v226, v227
	v_med3_f32 v228, v228, s6, v1
	v_med3_f32 v229, v229, s6, v1
	v_cvt_pk_fp8_f32 v200, v228, v229 op_sel:[0,0,1]
	v_mul_f32_e32 v226, 0x43800000, v115
	v_mul_f32_e32 v227, 0x43800000, v119
	v_med3_f32 v226, v226, s6, v1
	v_med3_f32 v227, v227, s6, v1
	v_mul_f32_e32 v228, 0x43800000, v123
	v_mul_f32_e32 v229, 0x43800000, v127
	v_cvt_pk_fp8_f32 v201, v226, v227
	v_med3_f32 v228, v228, s6, v1
	v_med3_f32 v229, v229, s6, v1
	v_cvt_pk_fp8_f32 v201, v228, v229 op_sel:[0,0,1]
	s_nop 1
	ds_write_b128 v232, v[198:201] offset:35088
	v_mul_f32_e32 v226, 0x43800000, v68
	v_mul_f32_e32 v227, 0x43800000, v72
	v_med3_f32 v226, v226, s6, v1
	v_med3_f32 v227, v227, s6, v1
	v_mul_f32_e32 v228, 0x43800000, v76
	v_mul_f32_e32 v229, 0x43800000, v80
	v_cvt_pk_fp8_f32 v202, v226, v227
	v_med3_f32 v228, v228, s6, v1
	v_med3_f32 v229, v229, s6, v1
	v_cvt_pk_fp8_f32 v202, v228, v229 op_sel:[0,0,1]
	v_mul_f32_e32 v226, 0x43800000, v84
	v_mul_f32_e32 v227, 0x43800000, v88
	v_med3_f32 v226, v226, s6, v1
	v_med3_f32 v227, v227, s6, v1
	v_mul_f32_e32 v228, 0x43800000, v92
	v_mul_f32_e32 v229, 0x43800000, v96
	v_cvt_pk_fp8_f32 v203, v226, v227
	v_med3_f32 v228, v228, s6, v1
	v_med3_f32 v229, v229, s6, v1
	v_cvt_pk_fp8_f32 v203, v228, v229 op_sel:[0,0,1]
	v_mul_f32_e32 v226, 0x43800000, v100
	v_mul_f32_e32 v227, 0x43800000, v104
	v_med3_f32 v226, v226, s6, v1
	v_med3_f32 v227, v227, s6, v1
	v_mul_f32_e32 v228, 0x43800000, v108
	v_mul_f32_e32 v229, 0x43800000, v112
	v_cvt_pk_fp8_f32 v204, v226, v227
	v_med3_f32 v228, v228, s6, v1
	v_med3_f32 v229, v229, s6, v1
	v_cvt_pk_fp8_f32 v204, v228, v229 op_sel:[0,0,1]
	v_mul_f32_e32 v226, 0x43800000, v116
	v_mul_f32_e32 v227, 0x43800000, v120
	v_med3_f32 v226, v226, s6, v1
	v_med3_f32 v227, v227, s6, v1
	v_mul_f32_e32 v228, 0x43800000, v124
	v_mul_f32_e32 v229, 0x43800000, v128
	v_cvt_pk_fp8_f32 v205, v226, v227
	v_med3_f32 v228, v228, s6, v1
	v_med3_f32 v229, v229, s6, v1
	v_cvt_pk_fp8_f32 v205, v228, v229 op_sel:[0,0,1]
	s_nop 1
	ds_write_b128 v232, v[202:205] offset:35360
	v_mul_f32_e32 v226, 0x43800000, v69
	v_mul_f32_e32 v227, 0x43800000, v73
	v_med3_f32 v226, v226, s6, v1
	v_med3_f32 v227, v227, s6, v1
	v_mul_f32_e32 v228, 0x43800000, v77
	v_mul_f32_e32 v229, 0x43800000, v81
	v_cvt_pk_fp8_f32 v206, v226, v227
	v_med3_f32 v228, v228, s6, v1
	v_med3_f32 v229, v229, s6, v1
	v_cvt_pk_fp8_f32 v206, v228, v229 op_sel:[0,0,1]
	v_mul_f32_e32 v226, 0x43800000, v85
	v_mul_f32_e32 v227, 0x43800000, v89
	v_med3_f32 v226, v226, s6, v1
	v_med3_f32 v227, v227, s6, v1
	v_mul_f32_e32 v228, 0x43800000, v93
	v_mul_f32_e32 v229, 0x43800000, v97
	v_cvt_pk_fp8_f32 v207, v226, v227
	v_med3_f32 v228, v228, s6, v1
	v_med3_f32 v229, v229, s6, v1
	v_cvt_pk_fp8_f32 v207, v228, v229 op_sel:[0,0,1]
	v_mul_f32_e32 v226, 0x43800000, v101
	v_mul_f32_e32 v227, 0x43800000, v105
	v_med3_f32 v226, v226, s6, v1
	v_med3_f32 v227, v227, s6, v1
	v_mul_f32_e32 v228, 0x43800000, v109
	v_mul_f32_e32 v229, 0x43800000, v113
	v_cvt_pk_fp8_f32 v208, v226, v227
	v_med3_f32 v228, v228, s6, v1
	v_med3_f32 v229, v229, s6, v1
	v_cvt_pk_fp8_f32 v208, v228, v229 op_sel:[0,0,1]
	v_mul_f32_e32 v226, 0x43800000, v117
	v_mul_f32_e32 v227, 0x43800000, v121
	v_med3_f32 v226, v226, s6, v1
	v_med3_f32 v227, v227, s6, v1
	v_mul_f32_e32 v228, 0x43800000, v125
	v_mul_f32_e32 v229, 0x43800000, v129
	v_cvt_pk_fp8_f32 v209, v226, v227
	v_med3_f32 v228, v228, s6, v1
	v_med3_f32 v229, v229, s6, v1
	v_cvt_pk_fp8_f32 v209, v228, v229 op_sel:[0,0,1]
	s_nop 1
	ds_write_b128 v232, v[206:209] offset:35632
	s_waitcnt lgkmcnt(0)
	s_barrier
	ds_read_b128 v[194:197], v233 offset:34816
	ds_read_b128 v[198:201], v233 offset:43520
	ds_read_b128 v[202:205], v233 offset:52224
	ds_read_b128 v[206:209], v233 offset:60928
	s_waitcnt lgkmcnt(3)
	global_store_dwordx4 v236, v[194:197], s[2:3] nt
	s_waitcnt lgkmcnt(2)
	global_store_dwordx4 v237, v[198:201], s[2:3] nt
	s_waitcnt lgkmcnt(1)
	global_store_dwordx4 v230, v[202:205], s[2:3] nt
	s_waitcnt lgkmcnt(0)
	global_store_dwordx4 v231, v[206:209], s[2:3] nt
	s_add_u32 s2, s2, 0x100
	s_addc_u32 s3, s3, 0
	s_barrier

.LBB0_990:
	s_cmp_eq_u32 s0, 0
	s_cselect_b64 s[0:1], -1, 0
	s_or_b64 s[0:1], s[0:1], s[10:11]
	s_mov_b64 s[6:7], -1
	s_and_b64 vcc, exec, s[0:1]
	s_cbranch_vccnz .LBB0_996
	s_barrier
	s_add_u32 s5, s74, 768
	s_lshr_b32 s4, s5, 5
	s_and_b32 s5, s5, 31
	v_readlane_b32 s0, v254, 6
	v_readlane_b32 s1, v254, 7
	s_lshl_b32 s6, s4, 25
	s_and_b32 s7, s5, 1
	s_lshl_b32 s7, s7, 13
	s_add_u32 s6, s6, s7
	s_lshr_b32 s7, s5, 1
	s_lshl_b32 s7, s7, 9
	s_add_u32 s6, s6, s7
	s_add_u32 s0, s0, s6
	s_addc_u32 s1, s1, 0
	s_lshl_b32 s6, s4, 23
	s_lshl_b32 s7, s5, 18
	s_add_u32 s6, s6, s7
	s_add_u32 s6, s6, 0x40000000
	s_add_u32 s2, s78, s6
	s_addc_u32 s3, s79, 0
	s_mov_b32 s6, 0xc3e00000
	v_mov_b32_e32 v1, 0x43e00000
	v_lshrrev_b32_e32 v226, 5, v0
	v_and_b32_e32 v227, 31, v0
	v_lshlrev_b32_e32 v228, 4, v227
	v_lshlrev_b32_e32 v229, 18, v226
	v_add_u32_e32 v250, v229, v228
	v_add_u32_e32 v251, 0x4000, v250
	v_add_u32_e32 v246, 0x8000, v250
	v_add_u32_e32 v247, 0xc000, v250
	v_add_u32_e32 v248, 0x10000, v250
	v_add_u32_e32 v249, 0x14000, v250
	v_add_u32_e32 v242, 0x18000, v250
	v_add_u32_e32 v243, 0x1c000, v250
	v_add_u32_e32 v244, 0x20000, v250
	v_add_u32_e32 v245, 0x24000, v250
	v_add_u32_e32 v238, 0x28000, v250
	v_add_u32_e32 v239, 0x2c000, v250
	v_add_u32_e32 v240, 0x30000, v250
	v_add_u32_e32 v241, 0x34000, v250
	v_add_u32_e32 v234, 0x38000, v250
	v_add_u32_e32 v235, 0x3c000, v250
	v_lshrrev_b32_e32 v194, 4, v0
	v_and_b32_e32 v195, 15, v0
	v_lshlrev_b32_e32 v236, 11, v194
	v_lshl_add_u32 v236, v195, 4, v236
	v_add_u32_e32 v237, 0x10000, v236
	v_add_u32_e32 v230, 0x20000, v236
	v_add_u32_e32 v231, 0x30000, v236
	v_mul_u32_u24_e32 v232, 0x440, v227
	v_lshl_add_u32 v232, v226, 4, v232
	v_mul_u32_u24_e32 v233, 0x110, v194
	v_lshl_add_u32 v233, v195, 4, v233
	global_load_dwordx4 v[2:5], v250, s[0:1] sc0 nt
	global_load_dwordx4 v[6:9], v251, s[0:1] sc0 nt
	global_load_dwordx4 v[10:13], v246, s[0:1] sc0 nt
	global_load_dwordx4 v[14:17], v247, s[0:1] sc0 nt
	global_load_dwordx4 v[18:21], v248, s[0:1] sc0 nt
	global_load_dwordx4 v[22:25], v249, s[0:1] sc0 nt
	global_load_dwordx4 v[26:29], v242, s[0:1] sc0 nt
	global_load_dwordx4 v[30:33], v243, s[0:1] sc0 nt
	global_load_dwordx4 v[34:37], v244, s[0:1] sc0 nt
	global_load_dwordx4 v[38:41], v245, s[0:1] sc0 nt
	global_load_dwordx4 v[42:45], v238, s[0:1] sc0 nt
	global_load_dwordx4 v[46:49], v239, s[0:1] sc0 nt
	global_load_dwordx4 v[50:53], v240, s[0:1] sc0 nt
	global_load_dwordx4 v[54:57], v241, s[0:1] sc0 nt
	global_load_dwordx4 v[58:61], v234, s[0:1] sc0 nt
	global_load_dwordx4 v[62:65], v235, s[0:1] sc0 nt
	s_add_u32 s0, s0, 0x400000
	s_addc_u32 s1, s1, 0
	global_load_dwordx4 v[66:69], v250, s[0:1] sc0 nt
	global_load_dwordx4 v[70:73], v251, s[0:1] sc0 nt
	global_load_dwordx4 v[74:77], v246, s[0:1] sc0 nt
	global_load_dwordx4 v[78:81], v247, s[0:1] sc0 nt
	global_load_dwordx4 v[82:85], v248, s[0:1] sc0 nt
	global_load_dwordx4 v[86:89], v249, s[0:1] sc0 nt
	global_load_dwordx4 v[90:93], v242, s[0:1] sc0 nt
	global_load_dwordx4 v[94:97], v243, s[0:1] sc0 nt
	global_load_dwordx4 v[98:101], v244, s[0:1] sc0 nt
	global_load_dwordx4 v[102:105], v245, s[0:1] sc0 nt
	global_load_dwordx4 v[106:109], v238, s[0:1] sc0 nt
	global_load_dwordx4 v[110:113], v239, s[0:1] sc0 nt
	global_load_dwordx4 v[114:117], v240, s[0:1] sc0 nt
	global_load_dwordx4 v[118:121], v241, s[0:1] sc0 nt
	global_load_dwordx4 v[122:125], v234, s[0:1] sc0 nt
	global_load_dwordx4 v[126:129], v235, s[0:1] sc0 nt
	s_add_u32 s0, s0, 0x400000
	s_addc_u32 s1, s1, 0
	global_load_dwordx4 v[130:133], v250, s[0:1] sc0 nt
	global_load_dwordx4 v[134:137], v251, s[0:1] sc0 nt
	global_load_dwordx4 v[138:141], v246, s[0:1] sc0 nt
	global_load_dwordx4 v[142:145], v247, s[0:1] sc0 nt
	global_load_dwordx4 v[146:149], v248, s[0:1] sc0 nt
	global_load_dwordx4 v[150:153], v249, s[0:1] sc0 nt
	global_load_dwordx4 v[154:157], v242, s[0:1] sc0 nt
	global_load_dwordx4 v[158:161], v243, s[0:1] sc0 nt
	global_load_dwordx4 v[162:165], v244, s[0:1] sc0 nt
	global_load_dwordx4 v[166:169], v245, s[0:1] sc0 nt
	global_load_dwordx4 v[170:173], v238, s[0:1] sc0 nt
	global_load_dwordx4 v[174:177], v239, s[0:1] sc0 nt
	global_load_dwordx4 v[178:181], v240, s[0:1] sc0 nt
	global_load_dwordx4 v[182:185], v241, s[0:1] sc0 nt
	global_load_dwordx4 v[186:189], v234, s[0:1] sc0 nt
	global_load_dwordx4 v[190:193], v235, s[0:1] sc0 nt
	s_add_u32 s0, s0, 0x400000
	s_addc_u32 s1, s1, 0
	s_waitcnt vmcnt(44)
	v_mul_f32_e32 v226, 0x43800000, v2
	v_mul_f32_e32 v227, 0x43800000, v6
	v_med3_f32 v226, v226, s6, v1
	v_med3_f32 v227, v227, s6, v1
	v_mul_f32_e32 v228, 0x43800000, v10
	v_mul_f32_e32 v229, 0x43800000, v14
	v_cvt_pk_fp8_f32 v194, v226, v227
	v_med3_f32 v228, v228, s6, v1
	v_med3_f32 v229, v229, s6, v1
	v_cvt_pk_fp8_f32 v194, v228, v229 op_sel:[0,0,1]
	s_waitcnt vmcnt(40)
	v_mul_f32_e32 v226, 0x43800000, v18
	v_mul_f32_e32 v227, 0x43800000, v22
	v_med3_f32 v226, v226, s6, v1
	v_med3_f32 v227, v227, s6, v1
	v_mul_f32_e32 v228, 0x43800000, v26
	v_mul_f32_e32 v229, 0x43800000, v30
	v_cvt_pk_fp8_f32 v195, v226, v227
	v_med3_f32 v228, v228, s6, v1
	v_med3_f32 v229, v229, s6, v1
	v_cvt_pk_fp8_f32 v195, v228, v229 op_sel:[0,0,1]
	s_waitcnt vmcnt(36)
	v_mul_f32_e32 v226, 0x43800000, v34
	v_mul_f32_e32 v227, 0x43800000, v38
	v_med3_f32 v226, v226, s6, v1
	v_med3_f32 v227, v227, s6, v1
	v_mul_f32_e32 v228, 0x43800000, v42
	v_mul_f32_e32 v229, 0x43800000, v46
	v_cvt_pk_fp8_f32 v196, v226, v227
	v_med3_f32 v228, v228, s6, v1
	v_med3_f32 v229, v229, s6, v1
	v_cvt_pk_fp8_f32 v196, v228, v229 op_sel:[0,0,1]
	s_waitcnt vmcnt(32)
	v_mul_f32_e32 v226, 0x43800000, v50
	v_mul_f32_e32 v227, 0x43800000, v54
	v_med3_f32 v226, v226, s6, v1
	v_med3_f32 v227, v227, s6, v1
	v_mul_f32_e32 v228, 0x43800000, v58
	v_mul_f32_e32 v229, 0x43800000, v62
	v_cvt_pk_fp8_f32 v197, v226, v227
	v_med3_f32 v228, v228, s6, v1
	v_med3_f32 v229, v229, s6, v1
	v_cvt_pk_fp8_f32 v197, v228, v229 op_sel:[0,0,1]
	s_nop 1
	ds_write_b128 v232, v[194:197] offset:0
	v_mul_f32_e32 v226, 0x43800000, v3
	v_mul_f32_e32 v227, 0x43800000, v7
	v_med3_f32 v226, v226, s6, v1
	v_med3_f32 v227, v227, s6, v1
	v_mul_f32_e32 v228, 0x43800000, v11
	v_mul_f32_e32 v229, 0x43800000, v15
	v_cvt_pk_fp8_f32 v198, v226, v227
	v_med3_f32 v228, v228, s6, v1
	v_med3_f32 v229, v229, s6, v1
	v_cvt_pk_fp8_f32 v198, v228, v229 op_sel:[0,0,1]
	v_mul_f32_e32 v226, 0x43800000, v19
	v_mul_f32_e32 v227, 0x43800000, v23
	v_med3_f32 v226, v226, s6, v1
	v_med3_f32 v227, v227, s6, v1
	v_mul_f32_e32 v228, 0x43800000, v27
	v_mul_f32_e32 v229, 0x43800000, v31
	v_cvt_pk_fp8_f32 v199, v226, v227
	v_med3_f32 v228, v228, s6, v1
	v_med3_f32 v229, v229, s6, v1
	v_cvt_pk_fp8_f32 v199, v228, v229 op_sel:[0,0,1]
	v_mul_f32_e32 v226, 0x43800000, v35
	v_mul_f32_e32 v227, 0x43800000, v39
	v_med3_f32 v226, v226, s6, v1
	v_med3_f32 v227, v227, s6, v1
	v_mul_f32_e32 v228, 0x43800000, v43
	v_mul_f32_e32 v229, 0x43800000, v47
	v_cvt_pk_fp8_f32 v200, v226, v227
	v_med3_f32 v228, v228, s6, v1
	v_med3_f32 v229, v229, s6, v1
	v_cvt_pk_fp8_f32 v200, v228, v229 op_sel:[0,0,1]
	v_mul_f32_e32 v226, 0x43800000, v51
	v_mul_f32_e32 v227, 0x43800000, v55
	v_med3_f32 v226, v226, s6, v1
	v_med3_f32 v227, v227, s6, v1
	v_mul_f32_e32 v228, 0x43800000, v59
	v_mul_f32_e32 v229, 0x43800000, v63
	v_cvt_pk_fp8_f32 v201, v226, v227
	v_med3_f32 v228, v228, s6, v1
	v_med3_f32 v229, v229, s6, v1
	v_cvt_pk_fp8_f32 v201, v228, v229 op_sel:[0,0,1]
	s_nop 1
	ds_write_b128 v232, v[198:201] offset:272
	v_mul_f32_e32 v226, 0x43800000, v4
	v_mul_f32_e32 v227, 0x43800000, v8
	v_med3_f32 v226, v226, s6, v1
	v_med3_f32 v227, v227, s6, v1
	v_mul_f32_e32 v228, 0x43800000, v12
	v_mul_f32_e32 v229, 0x43800000, v16
	v_cvt_pk_fp8_f32 v202, v226, v227
	v_med3_f32 v228, v228, s6, v1
	v_med3_f32 v229, v229, s6, v1
	v_cvt_pk_fp8_f32 v202, v228, v229 op_sel:[0,0,1]
	v_mul_f32_e32 v226, 0x43800000, v20
	v_mul_f32_e32 v227, 0x43800000, v24
	v_med3_f32 v226, v226, s6, v1
	v_med3_f32 v227, v227, s6, v1
	v_mul_f32_e32 v228, 0x43800000, v28
	v_mul_f32_e32 v229, 0x43800000, v32
	v_cvt_pk_fp8_f32 v203, v226, v227
	v_med3_f32 v228, v228, s6, v1
	v_med3_f32 v229, v229, s6, v1
	v_cvt_pk_fp8_f32 v203, v228, v229 op_sel:[0,0,1]
	v_mul_f32_e32 v226, 0x43800000, v36
	v_mul_f32_e32 v227, 0x43800000, v40
	v_med3_f32 v226, v226, s6, v1
	v_med3_f32 v227, v227, s6, v1
	v_mul_f32_e32 v228, 0x43800000, v44
	v_mul_f32_e32 v229, 0x43800000, v48
	v_cvt_pk_fp8_f32 v204, v226, v227
	v_med3_f32 v228, v228, s6, v1
	v_med3_f32 v229, v229, s6, v1
	v_cvt_pk_fp8_f32 v204, v228, v229 op_sel:[0,0,1]
	v_mul_f32_e32 v226, 0x43800000, v52
	v_mul_f32_e32 v227, 0x43800000, v56
	v_med3_f32 v226, v226, s6, v1
	v_med3_f32 v227, v227, s6, v1
	v_mul_f32_e32 v228, 0x43800000, v60
	v_mul_f32_e32 v229, 0x43800000, v64
	v_cvt_pk_fp8_f32 v205, v226, v227
	v_med3_f32 v228, v228, s6, v1
	v_med3_f32 v229, v229, s6, v1
	v_cvt_pk_fp8_f32 v205, v228, v229 op_sel:[0,0,1]
	s_nop 1
	ds_write_b128 v232, v[202:205] offset:544
	v_mul_f32_e32 v226, 0x43800000, v5
	v_mul_f32_e32 v227, 0x43800000, v9
	v_med3_f32 v226, v226, s6, v1
	v_med3_f32 v227, v227, s6, v1
	v_mul_f32_e32 v228, 0x43800000, v13
	v_mul_f32_e32 v229, 0x43800000, v17
	v_cvt_pk_fp8_f32 v206, v226, v227
	v_med3_f32 v228, v228, s6, v1
	v_med3_f32 v229, v229, s6, v1
	v_cvt_pk_fp8_f32 v206, v228, v229 op_sel:[0,0,1]
	v_mul_f32_e32 v226, 0x43800000, v21
	v_mul_f32_e32 v227, 0x43800000, v25
	v_med3_f32 v226, v226, s6, v1
	v_med3_f32 v227, v227, s6, v1
	v_mul_f32_e32 v228, 0x43800000, v29
	v_mul_f32_e32 v229, 0x43800000, v33
	v_cvt_pk_fp8_f32 v207, v226, v227
	v_med3_f32 v228, v228, s6, v1
	v_med3_f32 v229, v229, s6, v1
	v_cvt_pk_fp8_f32 v207, v228, v229 op_sel:[0,0,1]
	v_mul_f32_e32 v226, 0x43800000, v37
	v_mul_f32_e32 v227, 0x43800000, v41
	v_med3_f32 v226, v226, s6, v1
	v_med3_f32 v227, v227, s6, v1
	v_mul_f32_e32 v228, 0x43800000, v45
	v_mul_f32_e32 v229, 0x43800000, v49
	v_cvt_pk_fp8_f32 v208, v226, v227
	v_med3_f32 v228, v228, s6, v1
	v_med3_f32 v229, v229, s6, v1
	v_cvt_pk_fp8_f32 v208, v228, v229 op_sel:[0,0,1]
	v_mul_f32_e32 v226, 0x43800000, v53
	v_mul_f32_e32 v227, 0x43800000, v57
	v_med3_f32 v226, v226, s6, v1
	v_med3_f32 v227, v227, s6, v1
	v_mul_f32_e32 v228, 0x43800000, v61
	v_mul_f32_e32 v229, 0x43800000, v65
	v_cvt_pk_fp8_f32 v209, v226, v227
	v_med3_f32 v228, v228, s6, v1
	v_med3_f32 v229, v229, s6, v1
	v_cvt_pk_fp8_f32 v209, v228, v229 op_sel:[0,0,1]
	s_nop 1
	ds_write_b128 v232, v[206:209] offset:816
	s_waitcnt lgkmcnt(0)
	s_barrier
	global_load_dwordx4 v[2:5], v250, s[0:1] sc0 nt
	global_load_dwordx4 v[6:9], v251, s[0:1] sc0 nt
	global_load_dwordx4 v[10:13], v246, s[0:1] sc0 nt
	global_load_dwordx4 v[14:17], v247, s[0:1] sc0 nt
	global_load_dwordx4 v[18:21], v248, s[0:1] sc0 nt
	global_load_dwordx4 v[22:25], v249, s[0:1] sc0 nt
	global_load_dwordx4 v[26:29], v242, s[0:1] sc0 nt
	global_load_dwordx4 v[30:33], v243, s[0:1] sc0 nt
	global_load_dwordx4 v[34:37], v244, s[0:1] sc0 nt
	global_load_dwordx4 v[38:41], v245, s[0:1] sc0 nt
	global_load_dwordx4 v[42:45], v238, s[0:1] sc0 nt
	global_load_dwordx4 v[46:49], v239, s[0:1] sc0 nt
	global_load_dwordx4 v[50:53], v240, s[0:1] sc0 nt
	global_load_dwordx4 v[54:57], v241, s[0:1] sc0 nt
	global_load_dwordx4 v[58:61], v234, s[0:1] sc0 nt
	global_load_dwordx4 v[62:65], v235, s[0:1] sc0 nt
	s_add_u32 s0, s0, 0x400000
	s_addc_u32 s1, s1, 0
	ds_read_b128 v[194:197], v233 offset:0
	ds_read_b128 v[198:201], v233 offset:8704
	ds_read_b128 v[202:205], v233 offset:17408
	ds_read_b128 v[206:209], v233 offset:26112
	s_waitcnt lgkmcnt(3)
	global_store_dwordx4 v236, v[194:197], s[2:3] nt
	s_waitcnt lgkmcnt(2)
	global_store_dwordx4 v237, v[198:201], s[2:3] nt
	s_waitcnt lgkmcnt(1)
	global_store_dwordx4 v230, v[202:205], s[2:3] nt
	s_waitcnt lgkmcnt(0)
	global_store_dwordx4 v231, v[206:209], s[2:3] nt
	s_add_u32 s2, s2, 0x100
	s_addc_u32 s3, s3, 0
	s_waitcnt vmcnt(48)
	v_mul_f32_e32 v226, 0x43800000, v66
	v_mul_f32_e32 v227, 0x43800000, v70
	v_med3_f32 v226, v226, s6, v1
	v_med3_f32 v227, v227, s6, v1
	v_mul_f32_e32 v228, 0x43800000, v74
	v_mul_f32_e32 v229, 0x43800000, v78
	v_cvt_pk_fp8_f32 v194, v226, v227
	v_med3_f32 v228, v228, s6, v1
	v_med3_f32 v229, v229, s6, v1
	v_cvt_pk_fp8_f32 v194, v228, v229 op_sel:[0,0,1]
	s_waitcnt vmcnt(44)
	v_mul_f32_e32 v226, 0x43800000, v82
	v_mul_f32_e32 v227, 0x43800000, v86
	v_med3_f32 v226, v226, s6, v1
	v_med3_f32 v227, v227, s6, v1
	v_mul_f32_e32 v228, 0x43800000, v90
	v_mul_f32_e32 v229, 0x43800000, v94
	v_cvt_pk_fp8_f32 v195, v226, v227
	v_med3_f32 v228, v228, s6, v1
	v_med3_f32 v229, v229, s6, v1
	v_cvt_pk_fp8_f32 v195, v228, v229 op_sel:[0,0,1]
	s_waitcnt vmcnt(40)
	v_mul_f32_e32 v226, 0x43800000, v98
	v_mul_f32_e32 v227, 0x43800000, v102
	v_med3_f32 v226, v226, s6, v1
	v_med3_f32 v227, v227, s6, v1
	v_mul_f32_e32 v228, 0x43800000, v106
	v_mul_f32_e32 v229, 0x43800000, v110
	v_cvt_pk_fp8_f32 v196, v226, v227
	v_med3_f32 v228, v228, s6, v1
	v_med3_f32 v229, v229, s6, v1
	v_cvt_pk_fp8_f32 v196, v228, v229 op_sel:[0,0,1]
	s_waitcnt vmcnt(36)
	v_mul_f32_e32 v226, 0x43800000, v114
	v_mul_f32_e32 v227, 0x43800000, v118
	v_med3_f32 v226, v226, s6, v1
	v_med3_f32 v227, v227, s6, v1
	v_mul_f32_e32 v228, 0x43800000, v122
	v_mul_f32_e32 v229, 0x43800000, v126
	v_cvt_pk_fp8_f32 v197, v226, v227
	v_med3_f32 v228, v228, s6, v1
	v_med3_f32 v229, v229, s6, v1
	v_cvt_pk_fp8_f32 v197, v228, v229 op_sel:[0,0,1]
	s_nop 1
	ds_write_b128 v232, v[194:197] offset:34816
	v_mul_f32_e32 v226, 0x43800000, v67
	v_mul_f32_e32 v227, 0x43800000, v71
	v_med3_f32 v226, v226, s6, v1
	v_med3_f32 v227, v227, s6, v1
	v_mul_f32_e32 v228, 0x43800000, v75
	v_mul_f32_e32 v229, 0x43800000, v79
	v_cvt_pk_fp8_f32 v198, v226, v227
	v_med3_f32 v228, v228, s6, v1
	v_med3_f32 v229, v229, s6, v1
	v_cvt_pk_fp8_f32 v198, v228, v229 op_sel:[0,0,1]
	v_mul_f32_e32 v226, 0x43800000, v83
	v_mul_f32_e32 v227, 0x43800000, v87
	v_med3_f32 v226, v226, s6, v1
	v_med3_f32 v227, v227, s6, v1
	v_mul_f32_e32 v228, 0x43800000, v91
	v_mul_f32_e32 v229, 0x43800000, v95
	v_cvt_pk_fp8_f32 v199, v226, v227
	v_med3_f32 v228, v228, s6, v1
	v_med3_f32 v229, v229, s6, v1
	v_cvt_pk_fp8_f32 v199, v228, v229 op_sel:[0,0,1]
	v_mul_f32_e32 v226, 0x43800000, v99
	v_mul_f32_e32 v227, 0x43800000, v103
	v_med3_f32 v226, v226, s6, v1
	v_med3_f32 v227, v227, s6, v1
	v_mul_f32_e32 v228, 0x43800000, v107
	v_mul_f32_e32 v229, 0x43800000, v111
	v_cvt_pk_fp8_f32 v200, v226, v227
	v_med3_f32 v228, v228, s6, v1
	v_med3_f32 v229, v229, s6, v1
	v_cvt_pk_fp8_f32 v200, v228, v229 op_sel:[0,0,1]
	v_mul_f32_e32 v226, 0x43800000, v115
	v_mul_f32_e32 v227, 0x43800000, v119
	v_med3_f32 v226, v226, s6, v1
	v_med3_f32 v227, v227, s6, v1
	v_mul_f32_e32 v228, 0x43800000, v123
	v_mul_f32_e32 v229, 0x43800000, v127
	v_cvt_pk_fp8_f32 v201, v226, v227
	v_med3_f32 v228, v228, s6, v1
	v_med3_f32 v229, v229, s6, v1
	v_cvt_pk_fp8_f32 v201, v228, v229 op_sel:[0,0,1]
	s_nop 1
	ds_write_b128 v232, v[198:201] offset:35088
	v_mul_f32_e32 v226, 0x43800000, v68
	v_mul_f32_e32 v227, 0x43800000, v72
	v_med3_f32 v226, v226, s6, v1
	v_med3_f32 v227, v227, s6, v1
	v_mul_f32_e32 v228, 0x43800000, v76
	v_mul_f32_e32 v229, 0x43800000, v80
	v_cvt_pk_fp8_f32 v202, v226, v227
	v_med3_f32 v228, v228, s6, v1
	v_med3_f32 v229, v229, s6, v1
	v_cvt_pk_fp8_f32 v202, v228, v229 op_sel:[0,0,1]
	v_mul_f32_e32 v226, 0x43800000, v84
	v_mul_f32_e32 v227, 0x43800000, v88
	v_med3_f32 v226, v226, s6, v1
	v_med3_f32 v227, v227, s6, v1
	v_mul_f32_e32 v228, 0x43800000, v92
	v_mul_f32_e32 v229, 0x43800000, v96
	v_cvt_pk_fp8_f32 v203, v226, v227
	v_med3_f32 v228, v228, s6, v1
	v_med3_f32 v229, v229, s6, v1
	v_cvt_pk_fp8_f32 v203, v228, v229 op_sel:[0,0,1]
	v_mul_f32_e32 v226, 0x43800000, v100
	v_mul_f32_e32 v227, 0x43800000, v104
	v_med3_f32 v226, v226, s6, v1
	v_med3_f32 v227, v227, s6, v1
	v_mul_f32_e32 v228, 0x43800000, v108
	v_mul_f32_e32 v229, 0x43800000, v112
	v_cvt_pk_fp8_f32 v204, v226, v227
	v_med3_f32 v228, v228, s6, v1
	v_med3_f32 v229, v229, s6, v1
	v_cvt_pk_fp8_f32 v204, v228, v229 op_sel:[0,0,1]
	v_mul_f32_e32 v226, 0x43800000, v116
	v_mul_f32_e32 v227, 0x43800000, v120
	v_med3_f32 v226, v226, s6, v1
	v_med3_f32 v227, v227, s6, v1
	v_mul_f32_e32 v228, 0x43800000, v124
	v_mul_f32_e32 v229, 0x43800000, v128
	v_cvt_pk_fp8_f32 v205, v226, v227
	v_med3_f32 v228, v228, s6, v1
	v_med3_f32 v229, v229, s6, v1
	v_cvt_pk_fp8_f32 v205, v228, v229 op_sel:[0,0,1]
	s_nop 1
	ds_write_b128 v232, v[202:205] offset:35360
	v_mul_f32_e32 v226, 0x43800000, v69
	v_mul_f32_e32 v227, 0x43800000, v73
	v_med3_f32 v226, v226, s6, v1
	v_med3_f32 v227, v227, s6, v1
	v_mul_f32_e32 v228, 0x43800000, v77
	v_mul_f32_e32 v229, 0x43800000, v81
	v_cvt_pk_fp8_f32 v206, v226, v227
	v_med3_f32 v228, v228, s6, v1
	v_med3_f32 v229, v229, s6, v1
	v_cvt_pk_fp8_f32 v206, v228, v229 op_sel:[0,0,1]
	v_mul_f32_e32 v226, 0x43800000, v85
	v_mul_f32_e32 v227, 0x43800000, v89
	v_med3_f32 v226, v226, s6, v1
	v_med3_f32 v227, v227, s6, v1
	v_mul_f32_e32 v228, 0x43800000, v93
	v_mul_f32_e32 v229, 0x43800000, v97
	v_cvt_pk_fp8_f32 v207, v226, v227
	v_med3_f32 v228, v228, s6, v1
	v_med3_f32 v229, v229, s6, v1
	v_cvt_pk_fp8_f32 v207, v228, v229 op_sel:[0,0,1]
	v_mul_f32_e32 v226, 0x43800000, v101
	v_mul_f32_e32 v227, 0x43800000, v105
	v_med3_f32 v226, v226, s6, v1
	v_med3_f32 v227, v227, s6, v1
	v_mul_f32_e32 v228, 0x43800000, v109
	v_mul_f32_e32 v229, 0x43800000, v113
	v_cvt_pk_fp8_f32 v208, v226, v227
	v_med3_f32 v228, v228, s6, v1
	v_med3_f32 v229, v229, s6, v1
	v_cvt_pk_fp8_f32 v208, v228, v229 op_sel:[0,0,1]
	v_mul_f32_e32 v226, 0x43800000, v117
	v_mul_f32_e32 v227, 0x43800000, v121
	v_med3_f32 v226, v226, s6, v1
	v_med3_f32 v227, v227, s6, v1
	v_mul_f32_e32 v228, 0x43800000, v125
	v_mul_f32_e32 v229, 0x43800000, v129
	v_cvt_pk_fp8_f32 v209, v226, v227
	v_med3_f32 v228, v228, s6, v1
	v_med3_f32 v229, v229, s6, v1
	v_cvt_pk_fp8_f32 v209, v228, v229 op_sel:[0,0,1]
	s_nop 1
	ds_write_b128 v232, v[206:209] offset:35632
	s_waitcnt lgkmcnt(0)
	s_barrier
	global_load_dwordx4 v[66:69], v250, s[0:1] sc0 nt
	global_load_dwordx4 v[70:73], v251, s[0:1] sc0 nt
	global_load_dwordx4 v[74:77], v246, s[0:1] sc0 nt
	global_load_dwordx4 v[78:81], v247, s[0:1] sc0 nt
	global_load_dwordx4 v[82:85], v248, s[0:1] sc0 nt
	global_load_dwordx4 v[86:89], v249, s[0:1] sc0 nt
	global_load_dwordx4 v[90:93], v242, s[0:1] sc0 nt
	global_load_dwordx4 v[94:97], v243, s[0:1] sc0 nt
	global_load_dwordx4 v[98:101], v244, s[0:1] sc0 nt
	global_load_dwordx4 v[102:105], v245, s[0:1] sc0 nt
	global_load_dwordx4 v[106:109], v238, s[0:1] sc0 nt
	global_load_dwordx4 v[110:113], v239, s[0:1] sc0 nt
	global_load_dwordx4 v[114:117], v240, s[0:1] sc0 nt
	global_load_dwordx4 v[118:121], v241, s[0:1] sc0 nt
	global_load_dwordx4 v[122:125], v234, s[0:1] sc0 nt
	global_load_dwordx4 v[126:129], v235, s[0:1] sc0 nt
	s_add_u32 s0, s0, 0x400000
	s_addc_u32 s1, s1, 0
	ds_read_b128 v[194:197], v233 offset:34816
	ds_read_b128 v[198:201], v233 offset:43520
	ds_read_b128 v[202:205], v233 offset:52224
	ds_read_b128 v[206:209], v233 offset:60928
	s_waitcnt lgkmcnt(3)
	global_store_dwordx4 v236, v[194:197], s[2:3] nt
	s_waitcnt lgkmcnt(2)
	global_store_dwordx4 v237, v[198:201], s[2:3] nt
	s_waitcnt lgkmcnt(1)
	global_store_dwordx4 v230, v[202:205], s[2:3] nt
	s_waitcnt lgkmcnt(0)
	global_store_dwordx4 v231, v[206:209], s[2:3] nt
	s_add_u32 s2, s2, 0x100
	s_addc_u32 s3, s3, 0
	s_waitcnt vmcnt(52)
	v_mul_f32_e32 v226, 0x43800000, v130
	v_mul_f32_e32 v227, 0x43800000, v134
	v_med3_f32 v226, v226, s6, v1
	v_med3_f32 v227, v227, s6, v1
	v_mul_f32_e32 v228, 0x43800000, v138
	v_mul_f32_e32 v229, 0x43800000, v142
	v_cvt_pk_fp8_f32 v194, v226, v227
	v_med3_f32 v228, v228, s6, v1
	v_med3_f32 v229, v229, s6, v1
	v_cvt_pk_fp8_f32 v194, v228, v229 op_sel:[0,0,1]
	s_waitcnt vmcnt(48)
	v_mul_f32_e32 v226, 0x43800000, v146
	v_mul_f32_e32 v227, 0x43800000, v150
	v_med3_f32 v226, v226, s6, v1
	v_med3_f32 v227, v227, s6, v1
	v_mul_f32_e32 v228, 0x43800000, v154
	v_mul_f32_e32 v229, 0x43800000, v158
	v_cvt_pk_fp8_f32 v195, v226, v227
	v_med3_f32 v228, v228, s6, v1
	v_med3_f32 v229, v229, s6, v1
	v_cvt_pk_fp8_f32 v195, v228, v229 op_sel:[0,0,1]
	s_waitcnt vmcnt(44)
	v_mul_f32_e32 v226, 0x43800000, v162
	v_mul_f32_e32 v227, 0x43800000, v166
	v_med3_f32 v226, v226, s6, v1
	v_med3_f32 v227, v227, s6, v1
	v_mul_f32_e32 v228, 0x43800000, v170
	v_mul_f32_e32 v229, 0x43800000, v174
	v_cvt_pk_fp8_f32 v196, v226, v227
	v_med3_f32 v228, v228, s6, v1
	v_med3_f32 v229, v229, s6, v1
	v_cvt_pk_fp8_f32 v196, v228, v229 op_sel:[0,0,1]
	s_waitcnt vmcnt(40)
	v_mul_f32_e32 v226, 0x43800000, v178
	v_mul_f32_e32 v227, 0x43800000, v182
	v_med3_f32 v226, v226, s6, v1
	v_med3_f32 v227, v227, s6, v1
	v_mul_f32_e32 v228, 0x43800000, v186
	v_mul_f32_e32 v229, 0x43800000, v190
	v_cvt_pk_fp8_f32 v197, v226, v227
	v_med3_f32 v228, v228, s6, v1
	v_med3_f32 v229, v229, s6, v1
	v_cvt_pk_fp8_f32 v197, v228, v229 op_sel:[0,0,1]
	s_nop 1
	ds_write_b128 v232, v[194:197] offset:0
	v_mul_f32_e32 v226, 0x43800000, v131
	v_mul_f32_e32 v227, 0x43800000, v135
	v_med3_f32 v226, v226, s6, v1
	v_med3_f32 v227, v227, s6, v1
	v_mul_f32_e32 v228, 0x43800000, v139
	v_mul_f32_e32 v229, 0x43800000, v143
	v_cvt_pk_fp8_f32 v198, v226, v227
	v_med3_f32 v228, v228, s6, v1
	v_med3_f32 v229, v229, s6, v1
	v_cvt_pk_fp8_f32 v198, v228, v229 op_sel:[0,0,1]
	v_mul_f32_e32 v226, 0x43800000, v147
	v_mul_f32_e32 v227, 0x43800000, v151
	v_med3_f32 v226, v226, s6, v1
	v_med3_f32 v227, v227, s6, v1
	v_mul_f32_e32 v228, 0x43800000, v155
	v_mul_f32_e32 v229, 0x43800000, v159
	v_cvt_pk_fp8_f32 v199, v226, v227
	v_med3_f32 v228, v228, s6, v1
	v_med3_f32 v229, v229, s6, v1
	v_cvt_pk_fp8_f32 v199, v228, v229 op_sel:[0,0,1]
	v_mul_f32_e32 v226, 0x43800000, v163
	v_mul_f32_e32 v227, 0x43800000, v167
	v_med3_f32 v226, v226, s6, v1
	v_med3_f32 v227, v227, s6, v1
	v_mul_f32_e32 v228, 0x43800000, v171
	v_mul_f32_e32 v229, 0x43800000, v175
	v_cvt_pk_fp8_f32 v200, v226, v227
	v_med3_f32 v228, v228, s6, v1
	v_med3_f32 v229, v229, s6, v1
	v_cvt_pk_fp8_f32 v200, v228, v229 op_sel:[0,0,1]
	v_mul_f32_e32 v226, 0x43800000, v179
	v_mul_f32_e32 v227, 0x43800000, v183
	v_med3_f32 v226, v226, s6, v1
	v_med3_f32 v227, v227, s6, v1
	v_mul_f32_e32 v228, 0x43800000, v187
	v_mul_f32_e32 v229, 0x43800000, v191
	v_cvt_pk_fp8_f32 v201, v226, v227
	v_med3_f32 v228, v228, s6, v1
	v_med3_f32 v229, v229, s6, v1
	v_cvt_pk_fp8_f32 v201, v228, v229 op_sel:[0,0,1]
	s_nop 1
	ds_write_b128 v232, v[198:201] offset:272
	v_mul_f32_e32 v226, 0x43800000, v132
	v_mul_f32_e32 v227, 0x43800000, v136
	v_med3_f32 v226, v226, s6, v1
	v_med3_f32 v227, v227, s6, v1
	v_mul_f32_e32 v228, 0x43800000, v140
	v_mul_f32_e32 v229, 0x43800000, v144
	v_cvt_pk_fp8_f32 v202, v226, v227
	v_med3_f32 v228, v228, s6, v1
	v_med3_f32 v229, v229, s6, v1
	v_cvt_pk_fp8_f32 v202, v228, v229 op_sel:[0,0,1]
	v_mul_f32_e32 v226, 0x43800000, v148
	v_mul_f32_e32 v227, 0x43800000, v152
	v_med3_f32 v226, v226, s6, v1
	v_med3_f32 v227, v227, s6, v1
	v_mul_f32_e32 v228, 0x43800000, v156
	v_mul_f32_e32 v229, 0x43800000, v160
	v_cvt_pk_fp8_f32 v203, v226, v227
	v_med3_f32 v228, v228, s6, v1
	v_med3_f32 v229, v229, s6, v1
	v_cvt_pk_fp8_f32 v203, v228, v229 op_sel:[0,0,1]
	v_mul_f32_e32 v226, 0x43800000, v164
	v_mul_f32_e32 v227, 0x43800000, v168
	v_med3_f32 v226, v226, s6, v1
	v_med3_f32 v227, v227, s6, v1
	v_mul_f32_e32 v228, 0x43800000, v172
	v_mul_f32_e32 v229, 0x43800000, v176
	v_cvt_pk_fp8_f32 v204, v226, v227
	v_med3_f32 v228, v228, s6, v1
	v_med3_f32 v229, v229, s6, v1
	v_cvt_pk_fp8_f32 v204, v228, v229 op_sel:[0,0,1]
	v_mul_f32_e32 v226, 0x43800000, v180
	v_mul_f32_e32 v227, 0x43800000, v184
	v_med3_f32 v226, v226, s6, v1
	v_med3_f32 v227, v227, s6, v1
	v_mul_f32_e32 v228, 0x43800000, v188
	v_mul_f32_e32 v229, 0x43800000, v192
	v_cvt_pk_fp8_f32 v205, v226, v227
	v_med3_f32 v228, v228, s6, v1
	v_med3_f32 v229, v229, s6, v1
	v_cvt_pk_fp8_f32 v205, v228, v229 op_sel:[0,0,1]
	s_nop 1
	ds_write_b128 v232, v[202:205] offset:544
	v_mul_f32_e32 v226, 0x43800000, v133
	v_mul_f32_e32 v227, 0x43800000, v137
	v_med3_f32 v226, v226, s6, v1
	v_med3_f32 v227, v227, s6, v1
	v_mul_f32_e32 v228, 0x43800000, v141
	v_mul_f32_e32 v229, 0x43800000, v145
	v_cvt_pk_fp8_f32 v206, v226, v227
	v_med3_f32 v228, v228, s6, v1
	v_med3_f32 v229, v229, s6, v1
	v_cvt_pk_fp8_f32 v206, v228, v229 op_sel:[0,0,1]
	v_mul_f32_e32 v226, 0x43800000, v149
	v_mul_f32_e32 v227, 0x43800000, v153
	v_med3_f32 v226, v226, s6, v1
	v_med3_f32 v227, v227, s6, v1
	v_mul_f32_e32 v228, 0x43800000, v157
	v_mul_f32_e32 v229, 0x43800000, v161
	v_cvt_pk_fp8_f32 v207, v226, v227
	v_med3_f32 v228, v228, s6, v1
	v_med3_f32 v229, v229, s6, v1
	v_cvt_pk_fp8_f32 v207, v228, v229 op_sel:[0,0,1]
	v_mul_f32_e32 v226, 0x43800000, v165
	v_mul_f32_e32 v227, 0x43800000, v169
	v_med3_f32 v226, v226, s6, v1
	v_med3_f32 v227, v227, s6, v1
	v_mul_f32_e32 v228, 0x43800000, v173
	v_mul_f32_e32 v229, 0x43800000, v177
	v_cvt_pk_fp8_f32 v208, v226, v227
	v_med3_f32 v228, v228, s6, v1
	v_med3_f32 v229, v229, s6, v1
	v_cvt_pk_fp8_f32 v208, v228, v229 op_sel:[0,0,1]
	v_mul_f32_e32 v226, 0x43800000, v181
	v_mul_f32_e32 v227, 0x43800000, v185
	v_med3_f32 v226, v226, s6, v1
	v_med3_f32 v227, v227, s6, v1
	v_mul_f32_e32 v228, 0x43800000, v189
	v_mul_f32_e32 v229, 0x43800000, v193
	v_cvt_pk_fp8_f32 v209, v226, v227
	v_med3_f32 v228, v228, s6, v1
	v_med3_f32 v229, v229, s6, v1
	v_cvt_pk_fp8_f32 v209, v228, v229 op_sel:[0,0,1]
	s_nop 1
	ds_write_b128 v232, v[206:209] offset:816
	s_waitcnt lgkmcnt(0)
	s_barrier
	global_load_dwordx4 v[130:133], v250, s[0:1] sc0 nt
	global_load_dwordx4 v[134:137], v251, s[0:1] sc0 nt
	global_load_dwordx4 v[138:141], v246, s[0:1] sc0 nt
	global_load_dwordx4 v[142:145], v247, s[0:1] sc0 nt
	global_load_dwordx4 v[146:149], v248, s[0:1] sc0 nt
	global_load_dwordx4 v[150:153], v249, s[0:1] sc0 nt
	global_load_dwordx4 v[154:157], v242, s[0:1] sc0 nt
	global_load_dwordx4 v[158:161], v243, s[0:1] sc0 nt
	global_load_dwordx4 v[162:165], v244, s[0:1] sc0 nt
	global_load_dwordx4 v[166:169], v245, s[0:1] sc0 nt
	global_load_dwordx4 v[170:173], v238, s[0:1] sc0 nt
	global_load_dwordx4 v[174:177], v239, s[0:1] sc0 nt
	global_load_dwordx4 v[178:181], v240, s[0:1] sc0 nt
	global_load_dwordx4 v[182:185], v241, s[0:1] sc0 nt
	global_load_dwordx4 v[186:189], v234, s[0:1] sc0 nt
	global_load_dwordx4 v[190:193], v235, s[0:1] sc0 nt
	s_add_u32 s0, s0, 0x400000
	s_addc_u32 s1, s1, 0
	ds_read_b128 v[194:197], v233 offset:0
	ds_read_b128 v[198:201], v233 offset:8704
	ds_read_b128 v[202:205], v233 offset:17408
	ds_read_b128 v[206:209], v233 offset:26112
	s_waitcnt lgkmcnt(3)
	global_store_dwordx4 v236, v[194:197], s[2:3] nt
	s_waitcnt lgkmcnt(2)
	global_store_dwordx4 v237, v[198:201], s[2:3] nt
	s_waitcnt lgkmcnt(1)
	global_store_dwordx4 v230, v[202:205], s[2:3] nt
	s_waitcnt lgkmcnt(0)
	global_store_dwordx4 v231, v[206:209], s[2:3] nt
	s_add_u32 s2, s2, 0x100
	s_addc_u32 s3, s3, 0
	s_waitcnt vmcnt(56)
	v_mul_f32_e32 v226, 0x43800000, v2
	v_mul_f32_e32 v227, 0x43800000, v6
	v_med3_f32 v226, v226, s6, v1
	v_med3_f32 v227, v227, s6, v1
	v_mul_f32_e32 v228, 0x43800000, v10
	v_mul_f32_e32 v229, 0x43800000, v14
	v_cvt_pk_fp8_f32 v194, v226, v227
	v_med3_f32 v228, v228, s6, v1
	v_med3_f32 v229, v229, s6, v1
	v_cvt_pk_fp8_f32 v194, v228, v229 op_sel:[0,0,1]
	s_waitcnt vmcnt(52)
	v_mul_f32_e32 v226, 0x43800000, v18
	v_mul_f32_e32 v227, 0x43800000, v22
	v_med3_f32 v226, v226, s6, v1
	v_med3_f32 v227, v227, s6, v1
	v_mul_f32_e32 v228, 0x43800000, v26
	v_mul_f32_e32 v229, 0x43800000, v30
	v_cvt_pk_fp8_f32 v195, v226, v227
	v_med3_f32 v228, v228, s6, v1
	v_med3_f32 v229, v229, s6, v1
	v_cvt_pk_fp8_f32 v195, v228, v229 op_sel:[0,0,1]
	s_waitcnt vmcnt(48)
	v_mul_f32_e32 v226, 0x43800000, v34
	v_mul_f32_e32 v227, 0x43800000, v38
	v_med3_f32 v226, v226, s6, v1
	v_med3_f32 v227, v227, s6, v1
	v_mul_f32_e32 v228, 0x43800000, v42
	v_mul_f32_e32 v229, 0x43800000, v46
	v_cvt_pk_fp8_f32 v196, v226, v227
	v_med3_f32 v228, v228, s6, v1
	v_med3_f32 v229, v229, s6, v1
	v_cvt_pk_fp8_f32 v196, v228, v229 op_sel:[0,0,1]
	s_waitcnt vmcnt(44)
	v_mul_f32_e32 v226, 0x43800000, v50
	v_mul_f32_e32 v227, 0x43800000, v54
	v_med3_f32 v226, v226, s6, v1
	v_med3_f32 v227, v227, s6, v1
	v_mul_f32_e32 v228, 0x43800000, v58
	v_mul_f32_e32 v229, 0x43800000, v62
	v_cvt_pk_fp8_f32 v197, v226, v227
	v_med3_f32 v228, v228, s6, v1
	v_med3_f32 v229, v229, s6, v1
	v_cvt_pk_fp8_f32 v197, v228, v229 op_sel:[0,0,1]
	s_nop 1
	ds_write_b128 v232, v[194:197] offset:34816
	v_mul_f32_e32 v226, 0x43800000, v3
	v_mul_f32_e32 v227, 0x43800000, v7
	v_med3_f32 v226, v226, s6, v1
	v_med3_f32 v227, v227, s6, v1
	v_mul_f32_e32 v228, 0x43800000, v11
	v_mul_f32_e32 v229, 0x43800000, v15
	v_cvt_pk_fp8_f32 v198, v226, v227
	v_med3_f32 v228, v228, s6, v1
	v_med3_f32 v229, v229, s6, v1
	v_cvt_pk_fp8_f32 v198, v228, v229 op_sel:[0,0,1]
	v_mul_f32_e32 v226, 0x43800000, v19
	v_mul_f32_e32 v227, 0x43800000, v23
	v_med3_f32 v226, v226, s6, v1
	v_med3_f32 v227, v227, s6, v1
	v_mul_f32_e32 v228, 0x43800000, v27
	v_mul_f32_e32 v229, 0x43800000, v31
	v_cvt_pk_fp8_f32 v199, v226, v227
	v_med3_f32 v228, v228, s6, v1
	v_med3_f32 v229, v229, s6, v1
	v_cvt_pk_fp8_f32 v199, v228, v229 op_sel:[0,0,1]
	v_mul_f32_e32 v226, 0x43800000, v35
	v_mul_f32_e32 v227, 0x43800000, v39
	v_med3_f32 v226, v226, s6, v1
	v_med3_f32 v227, v227, s6, v1
	v_mul_f32_e32 v228, 0x43800000, v43
	v_mul_f32_e32 v229, 0x43800000, v47
	v_cvt_pk_fp8_f32 v200, v226, v227
	v_med3_f32 v228, v228, s6, v1
	v_med3_f32 v229, v229, s6, v1
	v_cvt_pk_fp8_f32 v200, v228, v229 op_sel:[0,0,1]
	v_mul_f32_e32 v226, 0x43800000, v51
	v_mul_f32_e32 v227, 0x43800000, v55
	v_med3_f32 v226, v226, s6, v1
	v_med3_f32 v227, v227, s6, v1
	v_mul_f32_e32 v228, 0x43800000, v59
	v_mul_f32_e32 v229, 0x43800000, v63
	v_cvt_pk_fp8_f32 v201, v226, v227
	v_med3_f32 v228, v228, s6, v1
	v_med3_f32 v229, v229, s6, v1
	v_cvt_pk_fp8_f32 v201, v228, v229 op_sel:[0,0,1]
	s_nop 1
	ds_write_b128 v232, v[198:201] offset:35088
	v_mul_f32_e32 v226, 0x43800000, v4
	v_mul_f32_e32 v227, 0x43800000, v8
	v_med3_f32 v226, v226, s6, v1
	v_med3_f32 v227, v227, s6, v1
	v_mul_f32_e32 v228, 0x43800000, v12
	v_mul_f32_e32 v229, 0x43800000, v16
	v_cvt_pk_fp8_f32 v202, v226, v227
	v_med3_f32 v228, v228, s6, v1
	v_med3_f32 v229, v229, s6, v1
	v_cvt_pk_fp8_f32 v202, v228, v229 op_sel:[0,0,1]
	v_mul_f32_e32 v226, 0x43800000, v20
	v_mul_f32_e32 v227, 0x43800000, v24
	v_med3_f32 v226, v226, s6, v1
	v_med3_f32 v227, v227, s6, v1
	v_mul_f32_e32 v228, 0x43800000, v28
	v_mul_f32_e32 v229, 0x43800000, v32
	v_cvt_pk_fp8_f32 v203, v226, v227
	v_med3_f32 v228, v228, s6, v1
	v_med3_f32 v229, v229, s6, v1
	v_cvt_pk_fp8_f32 v203, v228, v229 op_sel:[0,0,1]
	v_mul_f32_e32 v226, 0x43800000, v36
	v_mul_f32_e32 v227, 0x43800000, v40
	v_med3_f32 v226, v226, s6, v1
	v_med3_f32 v227, v227, s6, v1
	v_mul_f32_e32 v228, 0x43800000, v44
	v_mul_f32_e32 v229, 0x43800000, v48
	v_cvt_pk_fp8_f32 v204, v226, v227
	v_med3_f32 v228, v228, s6, v1
	v_med3_f32 v229, v229, s6, v1
	v_cvt_pk_fp8_f32 v204, v228, v229 op_sel:[0,0,1]
	v_mul_f32_e32 v226, 0x43800000, v52
	v_mul_f32_e32 v227, 0x43800000, v56
	v_med3_f32 v226, v226, s6, v1
	v_med3_f32 v227, v227, s6, v1
	v_mul_f32_e32 v228, 0x43800000, v60
	v_mul_f32_e32 v229, 0x43800000, v64
	v_cvt_pk_fp8_f32 v205, v226, v227
	v_med3_f32 v228, v228, s6, v1
	v_med3_f32 v229, v229, s6, v1
	v_cvt_pk_fp8_f32 v205, v228, v229 op_sel:[0,0,1]
	s_nop 1
	ds_write_b128 v232, v[202:205] offset:35360
	v_mul_f32_e32 v226, 0x43800000, v5
	v_mul_f32_e32 v227, 0x43800000, v9
	v_med3_f32 v226, v226, s6, v1
	v_med3_f32 v227, v227, s6, v1
	v_mul_f32_e32 v228, 0x43800000, v13
	v_mul_f32_e32 v229, 0x43800000, v17
	v_cvt_pk_fp8_f32 v206, v226, v227
	v_med3_f32 v228, v228, s6, v1
	v_med3_f32 v229, v229, s6, v1
	v_cvt_pk_fp8_f32 v206, v228, v229 op_sel:[0,0,1]
	v_mul_f32_e32 v226, 0x43800000, v21
	v_mul_f32_e32 v227, 0x43800000, v25
	v_med3_f32 v226, v226, s6, v1
	v_med3_f32 v227, v227, s6, v1
	v_mul_f32_e32 v228, 0x43800000, v29
	v_mul_f32_e32 v229, 0x43800000, v33
	v_cvt_pk_fp8_f32 v207, v226, v227
	v_med3_f32 v228, v228, s6, v1
	v_med3_f32 v229, v229, s6, v1
	v_cvt_pk_fp8_f32 v207, v228, v229 op_sel:[0,0,1]
	v_mul_f32_e32 v226, 0x43800000, v37
	v_mul_f32_e32 v227, 0x43800000, v41
	v_med3_f32 v226, v226, s6, v1
	v_med3_f32 v227, v227, s6, v1
	v_mul_f32_e32 v228, 0x43800000, v45
	v_mul_f32_e32 v229, 0x43800000, v49
	v_cvt_pk_fp8_f32 v208, v226, v227
	v_med3_f32 v228, v228, s6, v1
	v_med3_f32 v229, v229, s6, v1
	v_cvt_pk_fp8_f32 v208, v228, v229 op_sel:[0,0,1]
	v_mul_f32_e32 v226, 0x43800000, v53
	v_mul_f32_e32 v227, 0x43800000, v57
	v_med3_f32 v226, v226, s6, v1
	v_med3_f32 v227, v227, s6, v1
	v_mul_f32_e32 v228, 0x43800000, v61
	v_mul_f32_e32 v229, 0x43800000, v65
	v_cvt_pk_fp8_f32 v209, v226, v227
	v_med3_f32 v228, v228, s6, v1
	v_med3_f32 v229, v229, s6, v1
	v_cvt_pk_fp8_f32 v209, v228, v229 op_sel:[0,0,1]
	s_nop 1
	ds_write_b128 v232, v[206:209] offset:35632
	s_waitcnt lgkmcnt(0)
	s_barrier
	global_load_dwordx4 v[2:5], v250, s[0:1] sc0 nt
	global_load_dwordx4 v[6:9], v251, s[0:1] sc0 nt
	global_load_dwordx4 v[10:13], v246, s[0:1] sc0 nt
	global_load_dwordx4 v[14:17], v247, s[0:1] sc0 nt
	global_load_dwordx4 v[18:21], v248, s[0:1] sc0 nt
	global_load_dwordx4 v[22:25], v249, s[0:1] sc0 nt
	global_load_dwordx4 v[26:29], v242, s[0:1] sc0 nt
	global_load_dwordx4 v[30:33], v243, s[0:1] sc0 nt
	global_load_dwordx4 v[34:37], v244, s[0:1] sc0 nt
	global_load_dwordx4 v[38:41], v245, s[0:1] sc0 nt
	global_load_dwordx4 v[42:45], v238, s[0:1] sc0 nt
	global_load_dwordx4 v[46:49], v239, s[0:1] sc0 nt
	global_load_dwordx4 v[50:53], v240, s[0:1] sc0 nt
	global_load_dwordx4 v[54:57], v241, s[0:1] sc0 nt
	global_load_dwordx4 v[58:61], v234, s[0:1] sc0 nt
	global_load_dwordx4 v[62:65], v235, s[0:1] sc0 nt
	s_add_u32 s0, s0, 0x400000
	s_addc_u32 s1, s1, 0
	ds_read_b128 v[194:197], v233 offset:34816
	ds_read_b128 v[198:201], v233 offset:43520
	ds_read_b128 v[202:205], v233 offset:52224
	ds_read_b128 v[206:209], v233 offset:60928
	s_waitcnt lgkmcnt(3)
	global_store_dwordx4 v236, v[194:197], s[2:3] nt
	s_waitcnt lgkmcnt(2)
	global_store_dwordx4 v237, v[198:201], s[2:3] nt
	s_waitcnt lgkmcnt(1)
	global_store_dwordx4 v230, v[202:205], s[2:3] nt
	s_waitcnt lgkmcnt(0)
	global_store_dwordx4 v231, v[206:209], s[2:3] nt
	s_add_u32 s2, s2, 0x100
	s_addc_u32 s3, s3, 0
	s_waitcnt vmcnt(56)
	v_mul_f32_e32 v226, 0x43800000, v66
	v_mul_f32_e32 v227, 0x43800000, v70
	v_med3_f32 v226, v226, s6, v1
	v_med3_f32 v227, v227, s6, v1
	v_mul_f32_e32 v228, 0x43800000, v74
	v_mul_f32_e32 v229, 0x43800000, v78
	v_cvt_pk_fp8_f32 v194, v226, v227
	v_med3_f32 v228, v228, s6, v1
	v_med3_f32 v229, v229, s6, v1
	v_cvt_pk_fp8_f32 v194, v228, v229 op_sel:[0,0,1]
	s_waitcnt vmcnt(52)
	v_mul_f32_e32 v226, 0x43800000, v82
	v_mul_f32_e32 v227, 0x43800000, v86
	v_med3_f32 v226, v226, s6, v1
	v_med3_f32 v227, v227, s6, v1
	v_mul_f32_e32 v228, 0x43800000, v90
	v_mul_f32_e32 v229, 0x43800000, v94
	v_cvt_pk_fp8_f32 v195, v226, v227
	v_med3_f32 v228, v228, s6, v1
	v_med3_f32 v229, v229, s6, v1
	v_cvt_pk_fp8_f32 v195, v228, v229 op_sel:[0,0,1]
	s_waitcnt vmcnt(48)
	v_mul_f32_e32 v226, 0x43800000, v98
	v_mul_f32_e32 v227, 0x43800000, v102
	v_med3_f32 v226, v226, s6, v1
	v_med3_f32 v227, v227, s6, v1
	v_mul_f32_e32 v228, 0x43800000, v106
	v_mul_f32_e32 v229, 0x43800000, v110
	v_cvt_pk_fp8_f32 v196, v226, v227
	v_med3_f32 v228, v228, s6, v1
	v_med3_f32 v229, v229, s6, v1
	v_cvt_pk_fp8_f32 v196, v228, v229 op_sel:[0,0,1]
	s_waitcnt vmcnt(44)
	v_mul_f32_e32 v226, 0x43800000, v114
	v_mul_f32_e32 v227, 0x43800000, v118
	v_med3_f32 v226, v226, s6, v1
	v_med3_f32 v227, v227, s6, v1
	v_mul_f32_e32 v228, 0x43800000, v122
	v_mul_f32_e32 v229, 0x43800000, v126
	v_cvt_pk_fp8_f32 v197, v226, v227
	v_med3_f32 v228, v228, s6, v1
	v_med3_f32 v229, v229, s6, v1
	v_cvt_pk_fp8_f32 v197, v228, v229 op_sel:[0,0,1]
	s_nop 1
	ds_write_b128 v232, v[194:197] offset:0
	v_mul_f32_e32 v226, 0x43800000, v67
	v_mul_f32_e32 v227, 0x43800000, v71
	v_med3_f32 v226, v226, s6, v1
	v_med3_f32 v227, v227, s6, v1
	v_mul_f32_e32 v228, 0x43800000, v75
	v_mul_f32_e32 v229, 0x43800000, v79
	v_cvt_pk_fp8_f32 v198, v226, v227
	v_med3_f32 v228, v228, s6, v1
	v_med3_f32 v229, v229, s6, v1
	v_cvt_pk_fp8_f32 v198, v228, v229 op_sel:[0,0,1]
	v_mul_f32_e32 v226, 0x43800000, v83
	v_mul_f32_e32 v227, 0x43800000, v87
	v_med3_f32 v226, v226, s6, v1
	v_med3_f32 v227, v227, s6, v1
	v_mul_f32_e32 v228, 0x43800000, v91
	v_mul_f32_e32 v229, 0x43800000, v95
	v_cvt_pk_fp8_f32 v199, v226, v227
	v_med3_f32 v228, v228, s6, v1
	v_med3_f32 v229, v229, s6, v1
	v_cvt_pk_fp8_f32 v199, v228, v229 op_sel:[0,0,1]
	v_mul_f32_e32 v226, 0x43800000, v99
	v_mul_f32_e32 v227, 0x43800000, v103
	v_med3_f32 v226, v226, s6, v1
	v_med3_f32 v227, v227, s6, v1
	v_mul_f32_e32 v228, 0x43800000, v107
	v_mul_f32_e32 v229, 0x43800000, v111
	v_cvt_pk_fp8_f32 v200, v226, v227
	v_med3_f32 v228, v228, s6, v1
	v_med3_f32 v229, v229, s6, v1
	v_cvt_pk_fp8_f32 v200, v228, v229 op_sel:[0,0,1]
	v_mul_f32_e32 v226, 0x43800000, v115
	v_mul_f32_e32 v227, 0x43800000, v119
	v_med3_f32 v226, v226, s6, v1
	v_med3_f32 v227, v227, s6, v1
	v_mul_f32_e32 v228, 0x43800000, v123
	v_mul_f32_e32 v229, 0x43800000, v127
	v_cvt_pk_fp8_f32 v201, v226, v227
	v_med3_f32 v228, v228, s6, v1
	v_med3_f32 v229, v229, s6, v1
	v_cvt_pk_fp8_f32 v201, v228, v229 op_sel:[0,0,1]
	s_nop 1
	ds_write_b128 v232, v[198:201] offset:272
	v_mul_f32_e32 v226, 0x43800000, v68
	v_mul_f32_e32 v227, 0x43800000, v72
	v_med3_f32 v226, v226, s6, v1
	v_med3_f32 v227, v227, s6, v1
	v_mul_f32_e32 v228, 0x43800000, v76
	v_mul_f32_e32 v229, 0x43800000, v80
	v_cvt_pk_fp8_f32 v202, v226, v227
	v_med3_f32 v228, v228, s6, v1
	v_med3_f32 v229, v229, s6, v1
	v_cvt_pk_fp8_f32 v202, v228, v229 op_sel:[0,0,1]
	v_mul_f32_e32 v226, 0x43800000, v84
	v_mul_f32_e32 v227, 0x43800000, v88
	v_med3_f32 v226, v226, s6, v1
	v_med3_f32 v227, v227, s6, v1
	v_mul_f32_e32 v228, 0x43800000, v92
	v_mul_f32_e32 v229, 0x43800000, v96
	v_cvt_pk_fp8_f32 v203, v226, v227
	v_med3_f32 v228, v228, s6, v1
	v_med3_f32 v229, v229, s6, v1
	v_cvt_pk_fp8_f32 v203, v228, v229 op_sel:[0,0,1]
	v_mul_f32_e32 v226, 0x43800000, v100
	v_mul_f32_e32 v227, 0x43800000, v104
	v_med3_f32 v226, v226, s6, v1
	v_med3_f32 v227, v227, s6, v1
	v_mul_f32_e32 v228, 0x43800000, v108
	v_mul_f32_e32 v229, 0x43800000, v112
	v_cvt_pk_fp8_f32 v204, v226, v227
	v_med3_f32 v228, v228, s6, v1
	v_med3_f32 v229, v229, s6, v1
	v_cvt_pk_fp8_f32 v204, v228, v229 op_sel:[0,0,1]
	v_mul_f32_e32 v226, 0x43800000, v116
	v_mul_f32_e32 v227, 0x43800000, v120
	v_med3_f32 v226, v226, s6, v1
	v_med3_f32 v227, v227, s6, v1
	v_mul_f32_e32 v228, 0x43800000, v124
	v_mul_f32_e32 v229, 0x43800000, v128
	v_cvt_pk_fp8_f32 v205, v226, v227
	v_med3_f32 v228, v228, s6, v1
	v_med3_f32 v229, v229, s6, v1
	v_cvt_pk_fp8_f32 v205, v228, v229 op_sel:[0,0,1]
	s_nop 1
	ds_write_b128 v232, v[202:205] offset:544
	v_mul_f32_e32 v226, 0x43800000, v69
	v_mul_f32_e32 v227, 0x43800000, v73
	v_med3_f32 v226, v226, s6, v1
	v_med3_f32 v227, v227, s6, v1
	v_mul_f32_e32 v228, 0x43800000, v77
	v_mul_f32_e32 v229, 0x43800000, v81
	v_cvt_pk_fp8_f32 v206, v226, v227
	v_med3_f32 v228, v228, s6, v1
	v_med3_f32 v229, v229, s6, v1
	v_cvt_pk_fp8_f32 v206, v228, v229 op_sel:[0,0,1]
	v_mul_f32_e32 v226, 0x43800000, v85
	v_mul_f32_e32 v227, 0x43800000, v89
	v_med3_f32 v226, v226, s6, v1
	v_med3_f32 v227, v227, s6, v1
	v_mul_f32_e32 v228, 0x43800000, v93
	v_mul_f32_e32 v229, 0x43800000, v97
	v_cvt_pk_fp8_f32 v207, v226, v227
	v_med3_f32 v228, v228, s6, v1
	v_med3_f32 v229, v229, s6, v1
	v_cvt_pk_fp8_f32 v207, v228, v229 op_sel:[0,0,1]
	v_mul_f32_e32 v226, 0x43800000, v101
	v_mul_f32_e32 v227, 0x43800000, v105
	v_med3_f32 v226, v226, s6, v1
	v_med3_f32 v227, v227, s6, v1
	v_mul_f32_e32 v228, 0x43800000, v109
	v_mul_f32_e32 v229, 0x43800000, v113
	v_cvt_pk_fp8_f32 v208, v226, v227
	v_med3_f32 v228, v228, s6, v1
	v_med3_f32 v229, v229, s6, v1
	v_cvt_pk_fp8_f32 v208, v228, v229 op_sel:[0,0,1]
	v_mul_f32_e32 v226, 0x43800000, v117
	v_mul_f32_e32 v227, 0x43800000, v121
	v_med3_f32 v226, v226, s6, v1
	v_med3_f32 v227, v227, s6, v1
	v_mul_f32_e32 v228, 0x43800000, v125
	v_mul_f32_e32 v229, 0x43800000, v129
	v_cvt_pk_fp8_f32 v209, v226, v227
	v_med3_f32 v228, v228, s6, v1
	v_med3_f32 v229, v229, s6, v1
	v_cvt_pk_fp8_f32 v209, v228, v229 op_sel:[0,0,1]
	s_nop 1
	ds_write_b128 v232, v[206:209] offset:816
	s_waitcnt lgkmcnt(0)
	s_barrier
	global_load_dwordx4 v[66:69], v250, s[0:1] sc0 nt
	global_load_dwordx4 v[70:73], v251, s[0:1] sc0 nt
	global_load_dwordx4 v[74:77], v246, s[0:1] sc0 nt
	global_load_dwordx4 v[78:81], v247, s[0:1] sc0 nt
	global_load_dwordx4 v[82:85], v248, s[0:1] sc0 nt
	global_load_dwordx4 v[86:89], v249, s[0:1] sc0 nt
	global_load_dwordx4 v[90:93], v242, s[0:1] sc0 nt
	global_load_dwordx4 v[94:97], v243, s[0:1] sc0 nt
	global_load_dwordx4 v[98:101], v244, s[0:1] sc0 nt
	global_load_dwordx4 v[102:105], v245, s[0:1] sc0 nt
	global_load_dwordx4 v[106:109], v238, s[0:1] sc0 nt
	global_load_dwordx4 v[110:113], v239, s[0:1] sc0 nt
	global_load_dwordx4 v[114:117], v240, s[0:1] sc0 nt
	global_load_dwordx4 v[118:121], v241, s[0:1] sc0 nt
	global_load_dwordx4 v[122:125], v234, s[0:1] sc0 nt
	global_load_dwordx4 v[126:129], v235, s[0:1] sc0 nt
	s_add_u32 s0, s0, 0x400000
	s_addc_u32 s1, s1, 0
	ds_read_b128 v[194:197], v233 offset:0
	ds_read_b128 v[198:201], v233 offset:8704
	ds_read_b128 v[202:205], v233 offset:17408
	ds_read_b128 v[206:209], v233 offset:26112
	s_waitcnt lgkmcnt(3)
	global_store_dwordx4 v236, v[194:197], s[2:3] nt
	s_waitcnt lgkmcnt(2)
	global_store_dwordx4 v237, v[198:201], s[2:3] nt
	s_waitcnt lgkmcnt(1)
	global_store_dwordx4 v230, v[202:205], s[2:3] nt
	s_waitcnt lgkmcnt(0)
	global_store_dwordx4 v231, v[206:209], s[2:3] nt
	s_add_u32 s2, s2, 0x100
	s_addc_u32 s3, s3, 0
	s_waitcnt vmcnt(56)
	v_mul_f32_e32 v226, 0x43800000, v130
	v_mul_f32_e32 v227, 0x43800000, v134
	v_med3_f32 v226, v226, s6, v1
	v_med3_f32 v227, v227, s6, v1
	v_mul_f32_e32 v228, 0x43800000, v138
	v_mul_f32_e32 v229, 0x43800000, v142
	v_cvt_pk_fp8_f32 v194, v226, v227
	v_med3_f32 v228, v228, s6, v1
	v_med3_f32 v229, v229, s6, v1
	v_cvt_pk_fp8_f32 v194, v228, v229 op_sel:[0,0,1]
	s_waitcnt vmcnt(52)
	v_mul_f32_e32 v226, 0x43800000, v146
	v_mul_f32_e32 v227, 0x43800000, v150
	v_med3_f32 v226, v226, s6, v1
	v_med3_f32 v227, v227, s6, v1
	v_mul_f32_e32 v228, 0x43800000, v154
	v_mul_f32_e32 v229, 0x43800000, v158
	v_cvt_pk_fp8_f32 v195, v226, v227
	v_med3_f32 v228, v228, s6, v1
	v_med3_f32 v229, v229, s6, v1
	v_cvt_pk_fp8_f32 v195, v228, v229 op_sel:[0,0,1]
	s_waitcnt vmcnt(48)
	v_mul_f32_e32 v226, 0x43800000, v162
	v_mul_f32_e32 v227, 0x43800000, v166
	v_med3_f32 v226, v226, s6, v1
	v_med3_f32 v227, v227, s6, v1
	v_mul_f32_e32 v228, 0x43800000, v170
	v_mul_f32_e32 v229, 0x43800000, v174
	v_cvt_pk_fp8_f32 v196, v226, v227
	v_med3_f32 v228, v228, s6, v1
	v_med3_f32 v229, v229, s6, v1
	v_cvt_pk_fp8_f32 v196, v228, v229 op_sel:[0,0,1]
	s_waitcnt vmcnt(44)
	v_mul_f32_e32 v226, 0x43800000, v178
	v_mul_f32_e32 v227, 0x43800000, v182
	v_med3_f32 v226, v226, s6, v1
	v_med3_f32 v227, v227, s6, v1
	v_mul_f32_e32 v228, 0x43800000, v186
	v_mul_f32_e32 v229, 0x43800000, v190
	v_cvt_pk_fp8_f32 v197, v226, v227
	v_med3_f32 v228, v228, s6, v1
	v_med3_f32 v229, v229, s6, v1
	v_cvt_pk_fp8_f32 v197, v228, v229 op_sel:[0,0,1]
	s_nop 1
	ds_write_b128 v232, v[194:197] offset:34816
	v_mul_f32_e32 v226, 0x43800000, v131
	v_mul_f32_e32 v227, 0x43800000, v135
	v_med3_f32 v226, v226, s6, v1
	v_med3_f32 v227, v227, s6, v1
	v_mul_f32_e32 v228, 0x43800000, v139
	v_mul_f32_e32 v229, 0x43800000, v143
	v_cvt_pk_fp8_f32 v198, v226, v227
	v_med3_f32 v228, v228, s6, v1
	v_med3_f32 v229, v229, s6, v1
	v_cvt_pk_fp8_f32 v198, v228, v229 op_sel:[0,0,1]
	v_mul_f32_e32 v226, 0x43800000, v147
	v_mul_f32_e32 v227, 0x43800000, v151
	v_med3_f32 v226, v226, s6, v1
	v_med3_f32 v227, v227, s6, v1
	v_mul_f32_e32 v228, 0x43800000, v155
	v_mul_f32_e32 v229, 0x43800000, v159
	v_cvt_pk_fp8_f32 v199, v226, v227
	v_med3_f32 v228, v228, s6, v1
	v_med3_f32 v229, v229, s6, v1
	v_cvt_pk_fp8_f32 v199, v228, v229 op_sel:[0,0,1]
	v_mul_f32_e32 v226, 0x43800000, v163
	v_mul_f32_e32 v227, 0x43800000, v167
	v_med3_f32 v226, v226, s6, v1
	v_med3_f32 v227, v227, s6, v1
	v_mul_f32_e32 v228, 0x43800000, v171
	v_mul_f32_e32 v229, 0x43800000, v175
	v_cvt_pk_fp8_f32 v200, v226, v227
	v_med3_f32 v228, v228, s6, v1
	v_med3_f32 v229, v229, s6, v1
	v_cvt_pk_fp8_f32 v200, v228, v229 op_sel:[0,0,1]
	v_mul_f32_e32 v226, 0x43800000, v179
	v_mul_f32_e32 v227, 0x43800000, v183
	v_med3_f32 v226, v226, s6, v1
	v_med3_f32 v227, v227, s6, v1
	v_mul_f32_e32 v228, 0x43800000, v187
	v_mul_f32_e32 v229, 0x43800000, v191
	v_cvt_pk_fp8_f32 v201, v226, v227
	v_med3_f32 v228, v228, s6, v1
	v_med3_f32 v229, v229, s6, v1
	v_cvt_pk_fp8_f32 v201, v228, v229 op_sel:[0,0,1]
	s_nop 1
	ds_write_b128 v232, v[198:201] offset:35088
	v_mul_f32_e32 v226, 0x43800000, v132
	v_mul_f32_e32 v227, 0x43800000, v136
	v_med3_f32 v226, v226, s6, v1
	v_med3_f32 v227, v227, s6, v1
	v_mul_f32_e32 v228, 0x43800000, v140
	v_mul_f32_e32 v229, 0x43800000, v144
	v_cvt_pk_fp8_f32 v202, v226, v227
	v_med3_f32 v228, v228, s6, v1
	v_med3_f32 v229, v229, s6, v1
	v_cvt_pk_fp8_f32 v202, v228, v229 op_sel:[0,0,1]
	v_mul_f32_e32 v226, 0x43800000, v148
	v_mul_f32_e32 v227, 0x43800000, v152
	v_med3_f32 v226, v226, s6, v1
	v_med3_f32 v227, v227, s6, v1
	v_mul_f32_e32 v228, 0x43800000, v156
	v_mul_f32_e32 v229, 0x43800000, v160
	v_cvt_pk_fp8_f32 v203, v226, v227
	v_med3_f32 v228, v228, s6, v1
	v_med3_f32 v229, v229, s6, v1
	v_cvt_pk_fp8_f32 v203, v228, v229 op_sel:[0,0,1]
	v_mul_f32_e32 v226, 0x43800000, v164
	v_mul_f32_e32 v227, 0x43800000, v168
	v_med3_f32 v226, v226, s6, v1
	v_med3_f32 v227, v227, s6, v1
	v_mul_f32_e32 v228, 0x43800000, v172
	v_mul_f32_e32 v229, 0x43800000, v176
	v_cvt_pk_fp8_f32 v204, v226, v227
	v_med3_f32 v228, v228, s6, v1
	v_med3_f32 v229, v229, s6, v1
	v_cvt_pk_fp8_f32 v204, v228, v229 op_sel:[0,0,1]
	v_mul_f32_e32 v226, 0x43800000, v180
	v_mul_f32_e32 v227, 0x43800000, v184
	v_med3_f32 v226, v226, s6, v1
	v_med3_f32 v227, v227, s6, v1
	v_mul_f32_e32 v228, 0x43800000, v188
	v_mul_f32_e32 v229, 0x43800000, v192
	v_cvt_pk_fp8_f32 v205, v226, v227
	v_med3_f32 v228, v228, s6, v1
	v_med3_f32 v229, v229, s6, v1
	v_cvt_pk_fp8_f32 v205, v228, v229 op_sel:[0,0,1]
	s_nop 1
	ds_write_b128 v232, v[202:205] offset:35360
	v_mul_f32_e32 v226, 0x43800000, v133
	v_mul_f32_e32 v227, 0x43800000, v137
	v_med3_f32 v226, v226, s6, v1
	v_med3_f32 v227, v227, s6, v1
	v_mul_f32_e32 v228, 0x43800000, v141
	v_mul_f32_e32 v229, 0x43800000, v145
	v_cvt_pk_fp8_f32 v206, v226, v227
	v_med3_f32 v228, v228, s6, v1
	v_med3_f32 v229, v229, s6, v1
	v_cvt_pk_fp8_f32 v206, v228, v229 op_sel:[0,0,1]
	v_mul_f32_e32 v226, 0x43800000, v149
	v_mul_f32_e32 v227, 0x43800000, v153
	v_med3_f32 v226, v226, s6, v1
	v_med3_f32 v227, v227, s6, v1
	v_mul_f32_e32 v228, 0x43800000, v157
	v_mul_f32_e32 v229, 0x43800000, v161
	v_cvt_pk_fp8_f32 v207, v226, v227
	v_med3_f32 v228, v228, s6, v1
	v_med3_f32 v229, v229, s6, v1
	v_cvt_pk_fp8_f32 v207, v228, v229 op_sel:[0,0,1]
	v_mul_f32_e32 v226, 0x43800000, v165
	v_mul_f32_e32 v227, 0x43800000, v169
	v_med3_f32 v226, v226, s6, v1
	v_med3_f32 v227, v227, s6, v1
	v_mul_f32_e32 v228, 0x43800000, v173
	v_mul_f32_e32 v229, 0x43800000, v177
	v_cvt_pk_fp8_f32 v208, v226, v227
	v_med3_f32 v228, v228, s6, v1
	v_med3_f32 v229, v229, s6, v1
	v_cvt_pk_fp8_f32 v208, v228, v229 op_sel:[0,0,1]
	v_mul_f32_e32 v226, 0x43800000, v181
	v_mul_f32_e32 v227, 0x43800000, v185
	v_med3_f32 v226, v226, s6, v1
	v_med3_f32 v227, v227, s6, v1
	v_mul_f32_e32 v228, 0x43800000, v189
	v_mul_f32_e32 v229, 0x43800000, v193
	v_cvt_pk_fp8_f32 v209, v226, v227
	v_med3_f32 v228, v228, s6, v1
	v_med3_f32 v229, v229, s6, v1
	v_cvt_pk_fp8_f32 v209, v228, v229 op_sel:[0,0,1]
	s_nop 1
	ds_write_b128 v232, v[206:209] offset:35632
	s_waitcnt lgkmcnt(0)
	s_barrier
	ds_read_b128 v[194:197], v233 offset:34816
	ds_read_b128 v[198:201], v233 offset:43520
	ds_read_b128 v[202:205], v233 offset:52224
	ds_read_b128 v[206:209], v233 offset:60928
	s_waitcnt lgkmcnt(3)
	global_store_dwordx4 v236, v[194:197], s[2:3] nt
	s_waitcnt lgkmcnt(2)
	global_store_dwordx4 v237, v[198:201], s[2:3] nt
	s_waitcnt lgkmcnt(1)
	global_store_dwordx4 v230, v[202:205], s[2:3] nt
	s_waitcnt lgkmcnt(0)
	global_store_dwordx4 v231, v[206:209], s[2:3] nt
	s_add_u32 s2, s2, 0x100
	s_addc_u32 s3, s3, 0
	s_waitcnt vmcnt(40)
	v_mul_f32_e32 v226, 0x43800000, v2
	v_mul_f32_e32 v227, 0x43800000, v6
	v_med3_f32 v226, v226, s6, v1
	v_med3_f32 v227, v227, s6, v1
	v_mul_f32_e32 v228, 0x43800000, v10
	v_mul_f32_e32 v229, 0x43800000, v14
	v_cvt_pk_fp8_f32 v194, v226, v227
	v_med3_f32 v228, v228, s6, v1
	v_med3_f32 v229, v229, s6, v1
	v_cvt_pk_fp8_f32 v194, v228, v229 op_sel:[0,0,1]
	s_waitcnt vmcnt(36)
	v_mul_f32_e32 v226, 0x43800000, v18
	v_mul_f32_e32 v227, 0x43800000, v22
	v_med3_f32 v226, v226, s6, v1
	v_med3_f32 v227, v227, s6, v1
	v_mul_f32_e32 v228, 0x43800000, v26
	v_mul_f32_e32 v229, 0x43800000, v30
	v_cvt_pk_fp8_f32 v195, v226, v227
	v_med3_f32 v228, v228, s6, v1
	v_med3_f32 v229, v229, s6, v1
	v_cvt_pk_fp8_f32 v195, v228, v229 op_sel:[0,0,1]
	s_waitcnt vmcnt(32)
	v_mul_f32_e32 v226, 0x43800000, v34
	v_mul_f32_e32 v227, 0x43800000, v38
	v_med3_f32 v226, v226, s6, v1
	v_med3_f32 v227, v227, s6, v1
	v_mul_f32_e32 v228, 0x43800000, v42
	v_mul_f32_e32 v229, 0x43800000, v46
	v_cvt_pk_fp8_f32 v196, v226, v227
	v_med3_f32 v228, v228, s6, v1
	v_med3_f32 v229, v229, s6, v1
	v_cvt_pk_fp8_f32 v196, v228, v229 op_sel:[0,0,1]
	s_waitcnt vmcnt(28)
	v_mul_f32_e32 v226, 0x43800000, v50
	v_mul_f32_e32 v227, 0x43800000, v54
	v_med3_f32 v226, v226, s6, v1
	v_med3_f32 v227, v227, s6, v1
	v_mul_f32_e32 v228, 0x43800000, v58
	v_mul_f32_e32 v229, 0x43800000, v62
	v_cvt_pk_fp8_f32 v197, v226, v227
	v_med3_f32 v228, v228, s6, v1
	v_med3_f32 v229, v229, s6, v1
	v_cvt_pk_fp8_f32 v197, v228, v229 op_sel:[0,0,1]
	s_nop 1
	ds_write_b128 v232, v[194:197] offset:0
	v_mul_f32_e32 v226, 0x43800000, v3
	v_mul_f32_e32 v227, 0x43800000, v7
	v_med3_f32 v226, v226, s6, v1
	v_med3_f32 v227, v227, s6, v1
	v_mul_f32_e32 v228, 0x43800000, v11
	v_mul_f32_e32 v229, 0x43800000, v15
	v_cvt_pk_fp8_f32 v198, v226, v227
	v_med3_f32 v228, v228, s6, v1
	v_med3_f32 v229, v229, s6, v1
	v_cvt_pk_fp8_f32 v198, v228, v229 op_sel:[0,0,1]
	v_mul_f32_e32 v226, 0x43800000, v19
	v_mul_f32_e32 v227, 0x43800000, v23
	v_med3_f32 v226, v226, s6, v1
	v_med3_f32 v227, v227, s6, v1
	v_mul_f32_e32 v228, 0x43800000, v27
	v_mul_f32_e32 v229, 0x43800000, v31
	v_cvt_pk_fp8_f32 v199, v226, v227
	v_med3_f32 v228, v228, s6, v1
	v_med3_f32 v229, v229, s6, v1
	v_cvt_pk_fp8_f32 v199, v228, v229 op_sel:[0,0,1]
	v_mul_f32_e32 v226, 0x43800000, v35
	v_mul_f32_e32 v227, 0x43800000, v39
	v_med3_f32 v226, v226, s6, v1
	v_med3_f32 v227, v227, s6, v1
	v_mul_f32_e32 v228, 0x43800000, v43
	v_mul_f32_e32 v229, 0x43800000, v47
	v_cvt_pk_fp8_f32 v200, v226, v227
	v_med3_f32 v228, v228, s6, v1
	v_med3_f32 v229, v229, s6, v1
	v_cvt_pk_fp8_f32 v200, v228, v229 op_sel:[0,0,1]
	v_mul_f32_e32 v226, 0x43800000, v51
	v_mul_f32_e32 v227, 0x43800000, v55
	v_med3_f32 v226, v226, s6, v1
	v_med3_f32 v227, v227, s6, v1
	v_mul_f32_e32 v228, 0x43800000, v59
	v_mul_f32_e32 v229, 0x43800000, v63
	v_cvt_pk_fp8_f32 v201, v226, v227
	v_med3_f32 v228, v228, s6, v1
	v_med3_f32 v229, v229, s6, v1
	v_cvt_pk_fp8_f32 v201, v228, v229 op_sel:[0,0,1]
	s_nop 1
	ds_write_b128 v232, v[198:201] offset:272
	v_mul_f32_e32 v226, 0x43800000, v4
	v_mul_f32_e32 v227, 0x43800000, v8
	v_med3_f32 v226, v226, s6, v1
	v_med3_f32 v227, v227, s6, v1
	v_mul_f32_e32 v228, 0x43800000, v12
	v_mul_f32_e32 v229, 0x43800000, v16
	v_cvt_pk_fp8_f32 v202, v226, v227
	v_med3_f32 v228, v228, s6, v1
	v_med3_f32 v229, v229, s6, v1
	v_cvt_pk_fp8_f32 v202, v228, v229 op_sel:[0,0,1]
	v_mul_f32_e32 v226, 0x43800000, v20
	v_mul_f32_e32 v227, 0x43800000, v24
	v_med3_f32 v226, v226, s6, v1
	v_med3_f32 v227, v227, s6, v1
	v_mul_f32_e32 v228, 0x43800000, v28
	v_mul_f32_e32 v229, 0x43800000, v32
	v_cvt_pk_fp8_f32 v203, v226, v227
	v_med3_f32 v228, v228, s6, v1
	v_med3_f32 v229, v229, s6, v1
	v_cvt_pk_fp8_f32 v203, v228, v229 op_sel:[0,0,1]
	v_mul_f32_e32 v226, 0x43800000, v36
	v_mul_f32_e32 v227, 0x43800000, v40
	v_med3_f32 v226, v226, s6, v1
	v_med3_f32 v227, v227, s6, v1
	v_mul_f32_e32 v228, 0x43800000, v44
	v_mul_f32_e32 v229, 0x43800000, v48
	v_cvt_pk_fp8_f32 v204, v226, v227
	v_med3_f32 v228, v228, s6, v1
	v_med3_f32 v229, v229, s6, v1
	v_cvt_pk_fp8_f32 v204, v228, v229 op_sel:[0,0,1]
	v_mul_f32_e32 v226, 0x43800000, v52
	v_mul_f32_e32 v227, 0x43800000, v56
	v_med3_f32 v226, v226, s6, v1
	v_med3_f32 v227, v227, s6, v1
	v_mul_f32_e32 v228, 0x43800000, v60
	v_mul_f32_e32 v229, 0x43800000, v64
	v_cvt_pk_fp8_f32 v205, v226, v227
	v_med3_f32 v228, v228, s6, v1
	v_med3_f32 v229, v229, s6, v1
	v_cvt_pk_fp8_f32 v205, v228, v229 op_sel:[0,0,1]
	s_nop 1
	ds_write_b128 v232, v[202:205] offset:544
	v_mul_f32_e32 v226, 0x43800000, v5
	v_mul_f32_e32 v227, 0x43800000, v9
	v_med3_f32 v226, v226, s6, v1
	v_med3_f32 v227, v227, s6, v1
	v_mul_f32_e32 v228, 0x43800000, v13
	v_mul_f32_e32 v229, 0x43800000, v17
	v_cvt_pk_fp8_f32 v206, v226, v227
	v_med3_f32 v228, v228, s6, v1
	v_med3_f32 v229, v229, s6, v1
	v_cvt_pk_fp8_f32 v206, v228, v229 op_sel:[0,0,1]
	v_mul_f32_e32 v226, 0x43800000, v21
	v_mul_f32_e32 v227, 0x43800000, v25
	v_med3_f32 v226, v226, s6, v1
	v_med3_f32 v227, v227, s6, v1
	v_mul_f32_e32 v228, 0x43800000, v29
	v_mul_f32_e32 v229, 0x43800000, v33
	v_cvt_pk_fp8_f32 v207, v226, v227
	v_med3_f32 v228, v228, s6, v1
	v_med3_f32 v229, v229, s6, v1
	v_cvt_pk_fp8_f32 v207, v228, v229 op_sel:[0,0,1]
	v_mul_f32_e32 v226, 0x43800000, v37
	v_mul_f32_e32 v227, 0x43800000, v41
	v_med3_f32 v226, v226, s6, v1
	v_med3_f32 v227, v227, s6, v1
	v_mul_f32_e32 v228, 0x43800000, v45
	v_mul_f32_e32 v229, 0x43800000, v49
	v_cvt_pk_fp8_f32 v208, v226, v227
	v_med3_f32 v228, v228, s6, v1
	v_med3_f32 v229, v229, s6, v1
	v_cvt_pk_fp8_f32 v208, v228, v229 op_sel:[0,0,1]
	v_mul_f32_e32 v226, 0x43800000, v53
	v_mul_f32_e32 v227, 0x43800000, v57
	v_med3_f32 v226, v226, s6, v1
	v_med3_f32 v227, v227, s6, v1
	v_mul_f32_e32 v228, 0x43800000, v61
	v_mul_f32_e32 v229, 0x43800000, v65
	v_cvt_pk_fp8_f32 v209, v226, v227
	v_med3_f32 v228, v228, s6, v1
	v_med3_f32 v229, v229, s6, v1
	v_cvt_pk_fp8_f32 v209, v228, v229 op_sel:[0,0,1]
	s_nop 1
	ds_write_b128 v232, v[206:209] offset:816
	s_waitcnt lgkmcnt(0)
	s_barrier
	ds_read_b128 v[194:197], v233 offset:0
	ds_read_b128 v[198:201], v233 offset:8704
	ds_read_b128 v[202:205], v233 offset:17408
	ds_read_b128 v[206:209], v233 offset:26112
	s_waitcnt lgkmcnt(3)
	global_store_dwordx4 v236, v[194:197], s[2:3] nt
	s_waitcnt lgkmcnt(2)
	global_store_dwordx4 v237, v[198:201], s[2:3] nt
	s_waitcnt lgkmcnt(1)
	global_store_dwordx4 v230, v[202:205], s[2:3] nt
	s_waitcnt lgkmcnt(0)
	global_store_dwordx4 v231, v[206:209], s[2:3] nt
	s_add_u32 s2, s2, 0x100
	s_addc_u32 s3, s3, 0
	s_waitcnt vmcnt(24)
	v_mul_f32_e32 v226, 0x43800000, v66
	v_mul_f32_e32 v227, 0x43800000, v70
	v_med3_f32 v226, v226, s6, v1
	v_med3_f32 v227, v227, s6, v1
	v_mul_f32_e32 v228, 0x43800000, v74
	v_mul_f32_e32 v229, 0x43800000, v78
	v_cvt_pk_fp8_f32 v194, v226, v227
	v_med3_f32 v228, v228, s6, v1
	v_med3_f32 v229, v229, s6, v1
	v_cvt_pk_fp8_f32 v194, v228, v229 op_sel:[0,0,1]
	s_waitcnt vmcnt(20)
	v_mul_f32_e32 v226, 0x43800000, v82
	v_mul_f32_e32 v227, 0x43800000, v86
	v_med3_f32 v226, v226, s6, v1
	v_med3_f32 v227, v227, s6, v1
	v_mul_f32_e32 v228, 0x43800000, v90
	v_mul_f32_e32 v229, 0x43800000, v94
	v_cvt_pk_fp8_f32 v195, v226, v227
	v_med3_f32 v228, v228, s6, v1
	v_med3_f32 v229, v229, s6, v1
	v_cvt_pk_fp8_f32 v195, v228, v229 op_sel:[0,0,1]
	s_waitcnt vmcnt(16)
	v_mul_f32_e32 v226, 0x43800000, v98
	v_mul_f32_e32 v227, 0x43800000, v102
	v_med3_f32 v226, v226, s6, v1
	v_med3_f32 v227, v227, s6, v1
	v_mul_f32_e32 v228, 0x43800000, v106
	v_mul_f32_e32 v229, 0x43800000, v110
	v_cvt_pk_fp8_f32 v196, v226, v227
	v_med3_f32 v228, v228, s6, v1
	v_med3_f32 v229, v229, s6, v1
	v_cvt_pk_fp8_f32 v196, v228, v229 op_sel:[0,0,1]
	s_waitcnt vmcnt(12)
	v_mul_f32_e32 v226, 0x43800000, v114
	v_mul_f32_e32 v227, 0x43800000, v118
	v_med3_f32 v226, v226, s6, v1
	v_med3_f32 v227, v227, s6, v1
	v_mul_f32_e32 v228, 0x43800000, v122
	v_mul_f32_e32 v229, 0x43800000, v126
	v_cvt_pk_fp8_f32 v197, v226, v227
	v_med3_f32 v228, v228, s6, v1
	v_med3_f32 v229, v229, s6, v1
	v_cvt_pk_fp8_f32 v197, v228, v229 op_sel:[0,0,1]
	s_nop 1
	ds_write_b128 v232, v[194:197] offset:34816
	v_mul_f32_e32 v226, 0x43800000, v67
	v_mul_f32_e32 v227, 0x43800000, v71
	v_med3_f32 v226, v226, s6, v1
	v_med3_f32 v227, v227, s6, v1
	v_mul_f32_e32 v228, 0x43800000, v75
	v_mul_f32_e32 v229, 0x43800000, v79
	v_cvt_pk_fp8_f32 v198, v226, v227
	v_med3_f32 v228, v228, s6, v1
	v_med3_f32 v229, v229, s6, v1
	v_cvt_pk_fp8_f32 v198, v228, v229 op_sel:[0,0,1]
	v_mul_f32_e32 v226, 0x43800000, v83
	v_mul_f32_e32 v227, 0x43800000, v87
	v_med3_f32 v226, v226, s6, v1
	v_med3_f32 v227, v227, s6, v1
	v_mul_f32_e32 v228, 0x43800000, v91
	v_mul_f32_e32 v229, 0x43800000, v95
	v_cvt_pk_fp8_f32 v199, v226, v227
	v_med3_f32 v228, v228, s6, v1
	v_med3_f32 v229, v229, s6, v1
	v_cvt_pk_fp8_f32 v199, v228, v229 op_sel:[0,0,1]
	v_mul_f32_e32 v226, 0x43800000, v99
	v_mul_f32_e32 v227, 0x43800000, v103
	v_med3_f32 v226, v226, s6, v1
	v_med3_f32 v227, v227, s6, v1
	v_mul_f32_e32 v228, 0x43800000, v107
	v_mul_f32_e32 v229, 0x43800000, v111
	v_cvt_pk_fp8_f32 v200, v226, v227
	v_med3_f32 v228, v228, s6, v1
	v_med3_f32 v229, v229, s6, v1
	v_cvt_pk_fp8_f32 v200, v228, v229 op_sel:[0,0,1]
	v_mul_f32_e32 v226, 0x43800000, v115
	v_mul_f32_e32 v227, 0x43800000, v119
	v_med3_f32 v226, v226, s6, v1
	v_med3_f32 v227, v227, s6, v1
	v_mul_f32_e32 v228, 0x43800000, v123
	v_mul_f32_e32 v229, 0x43800000, v127
	v_cvt_pk_fp8_f32 v201, v226, v227
	v_med3_f32 v228, v228, s6, v1
	v_med3_f32 v229, v229, s6, v1
	v_cvt_pk_fp8_f32 v201, v228, v229 op_sel:[0,0,1]
	s_nop 1
	ds_write_b128 v232, v[198:201] offset:35088
	v_mul_f32_e32 v226, 0x43800000, v68
	v_mul_f32_e32 v227, 0x43800000, v72
	v_med3_f32 v226, v226, s6, v1
	v_med3_f32 v227, v227, s6, v1
	v_mul_f32_e32 v228, 0x43800000, v76
	v_mul_f32_e32 v229, 0x43800000, v80
	v_cvt_pk_fp8_f32 v202, v226, v227
	v_med3_f32 v228, v228, s6, v1
	v_med3_f32 v229, v229, s6, v1
	v_cvt_pk_fp8_f32 v202, v228, v229 op_sel:[0,0,1]
	v_mul_f32_e32 v226, 0x43800000, v84
	v_mul_f32_e32 v227, 0x43800000, v88
	v_med3_f32 v226, v226, s6, v1
	v_med3_f32 v227, v227, s6, v1
	v_mul_f32_e32 v228, 0x43800000, v92
	v_mul_f32_e32 v229, 0x43800000, v96
	v_cvt_pk_fp8_f32 v203, v226, v227
	v_med3_f32 v228, v228, s6, v1
	v_med3_f32 v229, v229, s6, v1
	v_cvt_pk_fp8_f32 v203, v228, v229 op_sel:[0,0,1]
	v_mul_f32_e32 v226, 0x43800000, v100
	v_mul_f32_e32 v227, 0x43800000, v104
	v_med3_f32 v226, v226, s6, v1
	v_med3_f32 v227, v227, s6, v1
	v_mul_f32_e32 v228, 0x43800000, v108
	v_mul_f32_e32 v229, 0x43800000, v112
	v_cvt_pk_fp8_f32 v204, v226, v227
	v_med3_f32 v228, v228, s6, v1
	v_med3_f32 v229, v229, s6, v1
	v_cvt_pk_fp8_f32 v204, v228, v229 op_sel:[0,0,1]
	v_mul_f32_e32 v226, 0x43800000, v116
	v_mul_f32_e32 v227, 0x43800000, v120
	v_med3_f32 v226, v226, s6, v1
	v_med3_f32 v227, v227, s6, v1
	v_mul_f32_e32 v228, 0x43800000, v124
	v_mul_f32_e32 v229, 0x43800000, v128
	v_cvt_pk_fp8_f32 v205, v226, v227
	v_med3_f32 v228, v228, s6, v1
	v_med3_f32 v229, v229, s6, v1
	v_cvt_pk_fp8_f32 v205, v228, v229 op_sel:[0,0,1]
	s_nop 1
	ds_write_b128 v232, v[202:205] offset:35360
	v_mul_f32_e32 v226, 0x43800000, v69
	v_mul_f32_e32 v227, 0x43800000, v73
	v_med3_f32 v226, v226, s6, v1
	v_med3_f32 v227, v227, s6, v1
	v_mul_f32_e32 v228, 0x43800000, v77
	v_mul_f32_e32 v229, 0x43800000, v81
	v_cvt_pk_fp8_f32 v206, v226, v227
	v_med3_f32 v228, v228, s6, v1
	v_med3_f32 v229, v229, s6, v1
	v_cvt_pk_fp8_f32 v206, v228, v229 op_sel:[0,0,1]
	v_mul_f32_e32 v226, 0x43800000, v85
	v_mul_f32_e32 v227, 0x43800000, v89
	v_med3_f32 v226, v226, s6, v1
	v_med3_f32 v227, v227, s6, v1
	v_mul_f32_e32 v228, 0x43800000, v93
	v_mul_f32_e32 v229, 0x43800000, v97
	v_cvt_pk_fp8_f32 v207, v226, v227
	v_med3_f32 v228, v228, s6, v1
	v_med3_f32 v229, v229, s6, v1
	v_cvt_pk_fp8_f32 v207, v228, v229 op_sel:[0,0,1]
	v_mul_f32_e32 v226, 0x43800000, v101
	v_mul_f32_e32 v227, 0x43800000, v105
	v_med3_f32 v226, v226, s6, v1
	v_med3_f32 v227, v227, s6, v1
	v_mul_f32_e32 v228, 0x43800000, v109
	v_mul_f32_e32 v229, 0x43800000, v113
	v_cvt_pk_fp8_f32 v208, v226, v227
	v_med3_f32 v228, v228, s6, v1
	v_med3_f32 v229, v229, s6, v1
	v_cvt_pk_fp8_f32 v208, v228, v229 op_sel:[0,0,1]
	v_mul_f32_e32 v226, 0x43800000, v117
	v_mul_f32_e32 v227, 0x43800000, v121
	v_med3_f32 v226, v226, s6, v1
	v_med3_f32 v227, v227, s6, v1
	v_mul_f32_e32 v228, 0x43800000, v125
	v_mul_f32_e32 v229, 0x43800000, v129
	v_cvt_pk_fp8_f32 v209, v226, v227
	v_med3_f32 v228, v228, s6, v1
	v_med3_f32 v229, v229, s6, v1
	v_cvt_pk_fp8_f32 v209, v228, v229 op_sel:[0,0,1]
	s_nop 1
	ds_write_b128 v232, v[206:209] offset:35632
	s_waitcnt lgkmcnt(0)
	s_barrier
	ds_read_b128 v[194:197], v233 offset:34816
	ds_read_b128 v[198:201], v233 offset:43520
	ds_read_b128 v[202:205], v233 offset:52224
	ds_read_b128 v[206:209], v233 offset:60928
	s_waitcnt lgkmcnt(3)
	global_store_dwordx4 v236, v[194:197], s[2:3] nt
	s_waitcnt lgkmcnt(2)
	global_store_dwordx4 v237, v[198:201], s[2:3] nt
	s_waitcnt lgkmcnt(1)
	global_store_dwordx4 v230, v[202:205], s[2:3] nt
	s_waitcnt lgkmcnt(0)
	global_store_dwordx4 v231, v[206:209], s[2:3] nt
	s_add_u32 s2, s2, 0x100
	s_addc_u32 s3, s3, 0
	s_barrier

.LBB0_1050:
	s_cmp_lt_i32 s96, 7
	s_cselect_b64 s[0:1], -1, 0
	s_and_b64 s[8:9], s[0:1], s[6:7]
	s_andn2_b64 vcc, exec, s[8:9]
	s_cbranch_vccnz .LBB0_1087
	v_readlane_b32 s2, v254, 55
	s_bitcmp1_b32 s74, 3
	v_readlane_b32 s3, v254, 56
	s_cselect_b64 s[0:1], -1, 0
	s_xor_b64 s[10:11], s[2:3], -1
	s_or_b64 s[0:1], s[0:1], s[10:11]
	s_mov_b64 s[6:7], -1
	s_and_b64 vcc, exec, s[0:1]
	s_branch .LBB0_1057
	s_cmp_gt_i32 s74, -1
	s_cbranch_scc0 .LBB0_1054
	s_lshr_b32 s0, s74, 4
	s_mov_b32 s1, 0
	v_readlane_b32 s12, v254, 4
	s_lshl_b64 s[2:3], s[0:1], 24
	v_readlane_b32 s18, v254, 10
	v_readlane_b32 s19, v254, 11
	s_add_u32 s2, s18, s2
	s_addc_u32 s3, s19, s3
	s_lshl_b32 s5, s74, 7
	s_and_b32 s5, s5, 0x380
	s_lshl_b32 s6, s5, 2
	s_add_u32 s2, s2, s6
	s_addc_u32 s3, s3, 0
	s_lshl_b64 s[0:1], s[0:1], 22
	s_lshl_b32 s5, s5, 11
	s_add_u32 s0, s78, s0
	v_mov_b32_e32 v134, v0
	s_addc_u32 s1, s79, s1
	s_add_u32 s6, s0, s5
	v_readfirstlane_b32 s4, v134
	s_addc_u32 s7, s1, 0
	s_ashr_i32 s0, s4, 1
	v_lshrrev_b32_e32 v1, 1, v134
	s_andn2_b32 s0, s0, 31
	v_and_b32_e32 v135, 16, v1
	s_waitcnt lgkmcnt(0)
	v_or_b32_e32 v2, s0, v135
	v_ashrrev_i32_e32 v3, 31, v2
	v_lshlrev_b32_e32 v1, 2, v134
	v_lshlrev_b64 v[2:3], 13, v[2:3]
	v_and_b32_e32 v140, 0x7c, v1
	v_lshl_add_u64 v[2:3], s[2:3], 0, v[2:3]
	v_lshlrev_b32_e32 v4, 2, v140
	v_mov_b32_e32 v5, 0
	v_lshl_add_u64 v[2:3], v[2:3], 0, v[4:5]
	s_movk_i32 s1, 0x2000
	v_add_co_u32_e32 v6, vcc, s1, v2
	s_movk_i32 s1, 0x4000
	s_nop 0
	v_addc_co_u32_e32 v7, vcc, 0, v3, vcc
	global_load_dwordx4 v[34:37], v[2:3], off sc0 nt
	global_load_dwordx4 v[38:41], v[6:7], off sc0 nt
	v_add_co_u32_e32 v6, vcc, s1, v2
	s_movk_i32 s1, 0x6000
	s_nop 0
	v_addc_co_u32_e32 v7, vcc, 0, v3, vcc
	v_add_co_u32_e32 v8, vcc, s1, v2
	s_mov_b32 s1, 0x8000
	s_nop 0
	v_addc_co_u32_e32 v9, vcc, 0, v3, vcc
	global_load_dwordx4 v[58:61], v[6:7], off sc0 nt
	global_load_dwordx4 v[50:53], v[8:9], off sc0 nt
	v_add_co_u32_e32 v6, vcc, s1, v2
	s_mov_b32 s1, 0xa000
	s_nop 0
	v_addc_co_u32_e32 v7, vcc, 0, v3, vcc
	v_add_co_u32_e32 v8, vcc, s1, v2
	s_mov_b32 s1, 0xc000
	s_nop 0
	v_addc_co_u32_e32 v9, vcc, 0, v3, vcc
	global_load_dwordx4 v[62:65], v[6:7], off sc0 nt
	global_load_dwordx4 v[70:73], v[8:9], off sc0 nt
	v_add_co_u32_e32 v6, vcc, s1, v2
	s_mov_b32 s1, 0xe000
	s_nop 0
	v_addc_co_u32_e32 v7, vcc, 0, v3, vcc
	v_add_co_u32_e32 v8, vcc, s1, v2
	s_mov_b32 s1, 0x10000
	s_nop 0
	v_addc_co_u32_e32 v9, vcc, 0, v3, vcc
	global_load_dwordx4 v[90:93], v[6:7], off sc0 nt
	global_load_dwordx4 v[74:77], v[8:9], off sc0 nt
	v_add_co_u32_e32 v6, vcc, s1, v2
	s_mov_b32 s1, 0x12000
	s_nop 0
	v_addc_co_u32_e32 v7, vcc, 0, v3, vcc
	v_add_co_u32_e32 v8, vcc, s1, v2
	s_mov_b32 s1, 0x14000
	s_nop 0
	v_addc_co_u32_e32 v9, vcc, 0, v3, vcc
	global_load_dwordx4 v[94:97], v[6:7], off sc0 nt
	global_load_dwordx4 v[98:101], v[8:9], off sc0 nt
	v_add_co_u32_e32 v6, vcc, s1, v2
	s_mov_b32 s1, 0x16000
	s_nop 0
	v_addc_co_u32_e32 v7, vcc, 0, v3, vcc
	v_add_co_u32_e32 v8, vcc, s1, v2
	s_mov_b32 s1, 0x18000
	s_nop 0
	v_addc_co_u32_e32 v9, vcc, 0, v3, vcc
	global_load_dwordx4 v[114:117], v[6:7], off sc0 nt
	global_load_dwordx4 v[106:109], v[8:9], off sc0 nt
	v_add_co_u32_e32 v6, vcc, s1, v2
	s_mov_b32 s1, 0x1a000
	s_nop 0
	v_addc_co_u32_e32 v7, vcc, 0, v3, vcc
	v_add_co_u32_e32 v8, vcc, s1, v2
	s_mov_b32 s1, 0x1c000
	s_nop 0
	v_addc_co_u32_e32 v9, vcc, 0, v3, vcc
	global_load_dwordx4 v[118:121], v[6:7], off sc0 nt
	global_load_dwordx4 v[122:125], v[8:9], off sc0 nt
	v_add_co_u32_e32 v6, vcc, s1, v2
	s_mov_b32 s1, 0x1e000
	s_nop 0
	v_addc_co_u32_e32 v7, vcc, 0, v3, vcc
	v_add_co_u32_e32 v8, vcc, s1, v2
	s_mov_b32 s1, 0x200000
	s_nop 0
	v_addc_co_u32_e32 v9, vcc, 0, v3, vcc
	v_add_co_u32_e32 v14, vcc, s1, v2
	s_mov_b32 s1, 0x202000
	s_nop 0
	v_addc_co_u32_e32 v15, vcc, 0, v3, vcc
	v_add_co_u32_e32 v16, vcc, s1, v2
	s_mov_b32 s1, 0x204000
	s_nop 0
	v_addc_co_u32_e32 v17, vcc, 0, v3, vcc
	v_add_co_u32_e32 v22, vcc, s1, v2
	s_mov_b32 s1, 0x206000
	s_nop 0
	v_addc_co_u32_e32 v23, vcc, 0, v3, vcc
	v_add_co_u32_e32 v24, vcc, s1, v2
	s_mov_b32 s1, 0x208000
	s_nop 0
	v_addc_co_u32_e32 v25, vcc, 0, v3, vcc
	v_add_co_u32_e32 v30, vcc, s1, v2
	s_mov_b32 s1, 0x20a000
	s_nop 0
	v_addc_co_u32_e32 v31, vcc, 0, v3, vcc
	v_add_co_u32_e32 v32, vcc, s1, v2
	s_mov_b32 s1, 0x20c000
	s_nop 0
	v_addc_co_u32_e32 v33, vcc, 0, v3, vcc
	s_waitcnt vmcnt(0)
	v_add_co_u32_e32 v46, vcc, s1, v2
	s_mov_b32 s1, 0x20e000
	s_nop 0
	v_addc_co_u32_e32 v47, vcc, 0, v3, vcc
	v_add_co_u32_e32 v48, vcc, s1, v2
	s_mov_b32 s1, 0x210000
	s_nop 0
	v_addc_co_u32_e32 v49, vcc, 0, v3, vcc
	v_add_co_u32_e32 v66, vcc, s1, v2
	s_mov_b32 s1, 0x212000
	s_nop 0
	v_addc_co_u32_e32 v67, vcc, 0, v3, vcc
	v_add_co_u32_e32 v68, vcc, s1, v2
	s_mov_b32 s1, 0x214000
	s_nop 0
	v_addc_co_u32_e32 v69, vcc, 0, v3, vcc
	v_add_co_u32_e32 v82, vcc, s1, v2
	s_mov_b32 s1, 0x216000
	s_nop 0
	v_addc_co_u32_e32 v83, vcc, 0, v3, vcc
	v_add_co_u32_e32 v84, vcc, s1, v2
	s_mov_b32 s1, 0x218000
	s_nop 0
	v_addc_co_u32_e32 v85, vcc, 0, v3, vcc
	global_load_dwordx4 v[130:133], v[6:7], off sc0 nt
	global_load_dwordx4 v[126:129], v[8:9], off sc0 nt
	s_nop 0
	global_load_dwordx4 v[6:9], v[14:15], off sc0 nt
	global_load_dwordx4 v[10:13], v[16:17], off sc0 nt
	global_load_dwordx4 v[18:21], v[22:23], off sc0 nt
	s_nop 0
	global_load_dwordx4 v[14:17], v[24:25], off sc0 nt
	s_nop 0
	global_load_dwordx4 v[22:25], v[30:31], off sc0 nt
	global_load_dwordx4 v[26:29], v[32:33], off sc0 nt
	global_load_dwordx4 v[42:45], v[46:47], off sc0 nt
	s_nop 0
	global_load_dwordx4 v[30:33], v[48:49], off sc0 nt
	s_nop 0
	global_load_dwordx4 v[46:49], v[66:67], off sc0 nt
	global_load_dwordx4 v[54:57], v[68:69], off sc0 nt
	global_load_dwordx4 v[78:81], v[82:83], off sc0 nt
	s_nop 0
	global_load_dwordx4 v[66:69], v[84:85], off sc0 nt
	v_add_co_u32_e32 v82, vcc, s1, v2
	s_mov_b32 s1, 0x21a000
	s_nop 0
	v_addc_co_u32_e32 v83, vcc, 0, v3, vcc
	v_add_co_u32_e32 v86, vcc, s1, v2
	s_mov_b32 s1, 0x21c000
	s_nop 0
	v_addc_co_u32_e32 v87, vcc, 0, v3, vcc
	v_add_co_u32_e32 v102, vcc, s1, v2
	s_mov_b32 s1, 0x21e000
	s_nop 0
	v_addc_co_u32_e32 v103, vcc, 0, v3, vcc
	v_add_co_u32_e32 v104, vcc, s1, v2
	global_load_dwordx4 v[82:85], v[82:83], off sc0 nt
	s_nop 0
	global_load_dwordx4 v[86:89], v[86:87], off sc0 nt
	v_addc_co_u32_e32 v105, vcc, 0, v3, vcc
	global_load_dwordx4 v[110:113], v[102:103], off sc0 nt
	s_nop 0
	global_load_dwordx4 v[102:105], v[104:105], off sc0 nt
	v_readlane_b32 s13, v254, 5
	v_readlane_b32 s14, v254, 6
	v_readlane_b32 s15, v254, 7
	v_readlane_b32 s16, v254, 8
	v_readlane_b32 s17, v254, 9
	s_add_i32 s2, s0, 0
	v_mul_f32_e32 v4, 0x43800000, v34
	v_mul_f32_e32 v34, 0x43800000, v38
	s_mov_b32 s0, 0xc3e00000
	v_mov_b32_e32 v1, 0x43e00000
	v_med3_f32 v4, v4, s0, v1
	v_med3_f32 v34, v34, s0, v1
	v_mov_b32_e32 v136, v5
	v_cvt_pk_fp8_f32 v136, v4, v34
	v_mul_f32_e32 v38, 0x43800000, v58
	v_mul_f32_e32 v4, 0x43800000, v50
	v_med3_f32 v34, v38, s0, v1
	v_med3_f32 v4, v4, s0, v1
	v_cvt_pk_fp8_f32 v136, v34, v4 op_sel:[0,0,1]
	v_mul_f32_e32 v4, 0x43800000, v62
	v_mul_f32_e32 v34, 0x43800000, v70
	v_med3_f32 v4, v4, s0, v1
	v_med3_f32 v34, v34, s0, v1
	v_mov_b32_e32 v137, v5
	v_cvt_pk_fp8_f32 v137, v4, v34
	v_mul_f32_e32 v38, 0x43800000, v90
	v_mul_f32_e32 v4, 0x43800000, v74
	v_med3_f32 v34, v38, s0, v1
	v_med3_f32 v4, v4, s0, v1
	v_cvt_pk_fp8_f32 v137, v34, v4 op_sel:[0,0,1]
	v_mul_f32_e32 v4, 0x43800000, v94
	v_mul_f32_e32 v34, 0x43800000, v98
	v_med3_f32 v4, v4, s0, v1
	v_med3_f32 v34, v34, s0, v1
	v_mov_b32_e32 v138, v5
	v_cvt_pk_fp8_f32 v138, v4, v34
	v_mul_f32_e32 v38, 0x43800000, v114
	v_mul_f32_e32 v4, 0x43800000, v106
	v_med3_f32 v34, v38, s0, v1
	v_med3_f32 v4, v4, s0, v1
	v_cvt_pk_fp8_f32 v138, v34, v4 op_sel:[0,0,1]
	v_mul_f32_e32 v4, 0x43800000, v118
	v_mul_f32_e32 v34, 0x43800000, v122
	v_med3_f32 v4, v4, s0, v1
	v_med3_f32 v34, v34, s0, v1
	v_mov_b32_e32 v139, v5
	v_cvt_pk_fp8_f32 v139, v4, v34
	s_waitcnt vmcnt(17)
	v_mul_f32_e32 v38, 0x43800000, v130
	s_waitcnt vmcnt(16)
	v_mul_f32_e32 v4, 0x43800000, v126
	v_med3_f32 v34, v38, s0, v1
	v_med3_f32 v4, v4, s0, v1
	v_cvt_pk_fp8_f32 v139, v34, v4 op_sel:[0,0,1]
	v_mul_u32_u24_e32 v4, 0x110, v140
	v_add3_u32 v166, s2, v135, v4
	v_mul_f32_e32 v4, 0x43800000, v35
	v_mul_f32_e32 v34, 0x43800000, v39
	v_med3_f32 v4, v4, s0, v1
	v_med3_f32 v34, v34, s0, v1
	v_mov_b32_e32 v140, v5
	v_cvt_pk_fp8_f32 v140, v4, v34
	v_mul_f32_e32 v35, 0x43800000, v59
	v_mul_f32_e32 v4, 0x43800000, v51
	v_med3_f32 v34, v35, s0, v1
	v_med3_f32 v4, v4, s0, v1
	v_cvt_pk_fp8_f32 v140, v34, v4 op_sel:[0,0,1]
	v_mul_f32_e32 v4, 0x43800000, v63
	v_mul_f32_e32 v34, 0x43800000, v71
	v_med3_f32 v4, v4, s0, v1
	v_med3_f32 v34, v34, s0, v1
	v_mov_b32_e32 v141, v5
	v_cvt_pk_fp8_f32 v141, v4, v34
	v_mul_f32_e32 v35, 0x43800000, v91
	v_mul_f32_e32 v4, 0x43800000, v75
	v_med3_f32 v34, v35, s0, v1
	v_med3_f32 v4, v4, s0, v1
	v_cvt_pk_fp8_f32 v141, v34, v4 op_sel:[0,0,1]
	v_mul_f32_e32 v4, 0x43800000, v95
	v_mul_f32_e32 v34, 0x43800000, v99
	v_med3_f32 v4, v4, s0, v1
	v_med3_f32 v34, v34, s0, v1
	v_mov_b32_e32 v142, v5
	v_cvt_pk_fp8_f32 v142, v4, v34
	v_mul_f32_e32 v35, 0x43800000, v115
	v_mul_f32_e32 v4, 0x43800000, v107
	v_med3_f32 v34, v35, s0, v1
	v_med3_f32 v4, v4, s0, v1
	v_cvt_pk_fp8_f32 v142, v34, v4 op_sel:[0,0,1]
	v_mul_f32_e32 v4, 0x43800000, v119
	v_mul_f32_e32 v34, 0x43800000, v123
	v_med3_f32 v4, v4, s0, v1
	v_med3_f32 v34, v34, s0, v1
	v_mov_b32_e32 v143, v5
	v_cvt_pk_fp8_f32 v143, v4, v34
	v_mul_f32_e32 v35, 0x43800000, v131
	v_mul_f32_e32 v4, 0x43800000, v127
	v_med3_f32 v34, v35, s0, v1
	v_med3_f32 v4, v4, s0, v1
	v_cvt_pk_fp8_f32 v143, v34, v4 op_sel:[0,0,1]
	v_mul_f32_e32 v4, 0x43800000, v36
	v_mul_f32_e32 v34, 0x43800000, v40
	v_med3_f32 v4, v4, s0, v1
	v_med3_f32 v34, v34, s0, v1
	v_mov_b32_e32 v144, v5
	v_cvt_pk_fp8_f32 v144, v4, v34
	v_mul_f32_e32 v35, 0x43800000, v60
	v_mul_f32_e32 v4, 0x43800000, v52
	v_med3_f32 v34, v35, s0, v1
	v_med3_f32 v4, v4, s0, v1
	v_cvt_pk_fp8_f32 v144, v34, v4 op_sel:[0,0,1]
	v_mul_f32_e32 v4, 0x43800000, v64
	v_mul_f32_e32 v34, 0x43800000, v72
	v_med3_f32 v4, v4, s0, v1
	v_med3_f32 v34, v34, s0, v1
	v_mov_b32_e32 v145, v5
	v_cvt_pk_fp8_f32 v145, v4, v34
	v_mul_f32_e32 v35, 0x43800000, v92
	v_mul_f32_e32 v4, 0x43800000, v76
	v_med3_f32 v34, v35, s0, v1
	v_med3_f32 v4, v4, s0, v1
	v_cvt_pk_fp8_f32 v145, v34, v4 op_sel:[0,0,1]
	v_mul_f32_e32 v4, 0x43800000, v96
	v_mul_f32_e32 v34, 0x43800000, v100
	v_med3_f32 v4, v4, s0, v1
	v_med3_f32 v34, v34, s0, v1
	v_mov_b32_e32 v146, v5
	v_cvt_pk_fp8_f32 v146, v4, v34
	v_mul_f32_e32 v35, 0x43800000, v116
	v_mul_f32_e32 v4, 0x43800000, v108
	v_med3_f32 v34, v35, s0, v1
	v_med3_f32 v4, v4, s0, v1
	v_cvt_pk_fp8_f32 v146, v34, v4 op_sel:[0,0,1]
	v_mul_f32_e32 v4, 0x43800000, v120
	v_mul_f32_e32 v34, 0x43800000, v124
	v_med3_f32 v4, v4, s0, v1
	v_med3_f32 v34, v34, s0, v1
	v_mov_b32_e32 v147, v5
	v_cvt_pk_fp8_f32 v147, v4, v34
	v_mul_f32_e32 v35, 0x43800000, v132
	v_mul_f32_e32 v4, 0x43800000, v128
	v_med3_f32 v34, v35, s0, v1
	v_med3_f32 v4, v4, s0, v1
	v_cvt_pk_fp8_f32 v147, v34, v4 op_sel:[0,0,1]
	v_mul_f32_e32 v4, 0x43800000, v37
	v_mul_f32_e32 v34, 0x43800000, v41
	v_med3_f32 v4, v4, s0, v1
	v_med3_f32 v36, v34, s0, v1
	v_mov_b32_e32 v34, v5
	v_cvt_pk_fp8_f32 v34, v4, v36
	v_mul_f32_e32 v35, 0x43800000, v61
	v_mul_f32_e32 v4, 0x43800000, v53
	v_med3_f32 v35, v35, s0, v1
	v_med3_f32 v4, v4, s0, v1
	v_cvt_pk_fp8_f32 v34, v35, v4 op_sel:[0,0,1]
	v_mul_f32_e32 v4, 0x43800000, v65
	v_mul_f32_e32 v35, 0x43800000, v73
	v_med3_f32 v4, v4, s0, v1
	v_med3_f32 v37, v35, s0, v1
	v_mov_b32_e32 v35, v5
	v_cvt_pk_fp8_f32 v35, v4, v37
	v_mul_f32_e32 v36, 0x43800000, v93
	v_mul_f32_e32 v4, 0x43800000, v77
	v_med3_f32 v36, v36, s0, v1
	v_med3_f32 v4, v4, s0, v1
	v_cvt_pk_fp8_f32 v35, v36, v4 op_sel:[0,0,1]
	v_mul_f32_e32 v4, 0x43800000, v97
	v_mul_f32_e32 v36, 0x43800000, v101
	v_med3_f32 v4, v4, s0, v1
	v_med3_f32 v38, v36, s0, v1
	v_mov_b32_e32 v36, v5
	v_cvt_pk_fp8_f32 v36, v4, v38
	v_mul_f32_e32 v37, 0x43800000, v117
	v_mul_f32_e32 v4, 0x43800000, v109
	v_med3_f32 v37, v37, s0, v1
	v_med3_f32 v4, v4, s0, v1
	v_cvt_pk_fp8_f32 v36, v37, v4 op_sel:[0,0,1]
	v_mul_f32_e32 v4, 0x43800000, v121
	v_mul_f32_e32 v37, 0x43800000, v125
	v_med3_f32 v4, v4, s0, v1
	v_med3_f32 v39, v37, s0, v1
	v_mov_b32_e32 v37, v5
	v_cvt_pk_fp8_f32 v37, v4, v39
	v_mul_f32_e32 v38, 0x43800000, v133
	v_mul_f32_e32 v4, 0x43800000, v129
	v_med3_f32 v38, v38, s0, v1
	v_med3_f32 v4, v4, s0, v1
	v_cvt_pk_fp8_f32 v37, v38, v4 op_sel:[0,0,1]
	ds_write_b128 v166, v[136:139]
	ds_write_b128 v166, v[140:143] offset:272
	ds_write_b128 v166, v[144:147] offset:544
	ds_write_b128 v166, v[34:37] offset:816
	v_add_u32_e32 v34, 0x200, v134
	v_ashrrev_i32_e32 v140, 4, v34
	v_add_u32_e32 v34, 0x400, v134
	v_ashrrev_i32_e32 v144, 4, v34
	v_add_u32_e32 v34, 0x600, v134
	v_ashrrev_i32_e32 v136, 4, v134
	v_ashrrev_i32_e32 v148, 4, v34
	v_lshlrev_b32_e32 v4, 4, v134
	v_ashrrev_i32_e32 v137, 31, v136
	v_ashrrev_i32_e32 v141, 31, v140
	v_ashrrev_i32_e32 v145, 31, v144
	v_ashrrev_i32_e32 v149, 31, v148
	s_movk_i32 s1, 0x110
	s_waitcnt lgkmcnt(0)
	s_barrier
	v_and_b32_e32 v4, 0xf0, v4
	v_lshlrev_b64 v[138:139], 11, v[136:137]
	v_lshlrev_b64 v[142:143], 11, v[140:141]
	v_lshlrev_b64 v[146:147], 11, v[144:145]
	v_lshlrev_b64 v[164:165], 11, v[148:149]
	s_mov_b32 s2, 0x400000
	v_add_co_u32_e32 v34, vcc, s2, v2
	s_mov_b32 s2, 0x402000
	s_nop 0
	v_addc_co_u32_e32 v35, vcc, 0, v3, vcc
	v_add_co_u32_e32 v38, vcc, s2, v2
	s_mov_b32 s2, 0x404000
	s_nop 0
	v_addc_co_u32_e32 v39, vcc, 0, v3, vcc
	v_add_co_u32_e32 v50, vcc, s2, v2
	s_mov_b32 s2, 0x406000
	s_nop 0
	v_addc_co_u32_e32 v51, vcc, 0, v3, vcc
	v_add_co_u32_e32 v52, vcc, s2, v2
	s_mov_b32 s2, 0x408000
	s_nop 0
	v_addc_co_u32_e32 v53, vcc, 0, v3, vcc
	v_add_co_u32_e32 v62, vcc, s2, v2
	s_mov_b32 s2, 0x40a000
	s_nop 0
	v_addc_co_u32_e32 v63, vcc, 0, v3, vcc
	v_add_co_u32_e32 v70, vcc, s2, v2
	s_mov_b32 s2, 0x40c000
	s_nop 0
	v_addc_co_u32_e32 v71, vcc, 0, v3, vcc
	v_add_co_u32_e32 v74, vcc, s2, v2
	s_mov_b32 s2, 0x40e000
	s_nop 0
	v_addc_co_u32_e32 v75, vcc, 0, v3, vcc
	v_add_co_u32_e32 v76, vcc, s2, v2
	s_mov_b32 s2, 0x410000
	s_nop 0
	v_addc_co_u32_e32 v77, vcc, 0, v3, vcc
	v_add_co_u32_e32 v94, vcc, s2, v2
	s_mov_b32 s2, 0x412000
	s_nop 0
	v_addc_co_u32_e32 v95, vcc, 0, v3, vcc
	v_add_co_u32_e32 v98, vcc, s2, v2
	s_mov_b32 s2, 0x414000
	s_nop 0
	v_addc_co_u32_e32 v99, vcc, 0, v3, vcc
	v_add_co_u32_e32 v106, vcc, s2, v2
	s_mov_b32 s2, 0x416000
	s_nop 0
	v_addc_co_u32_e32 v107, vcc, 0, v3, vcc
	v_add_co_u32_e32 v108, vcc, s2, v2
	s_mov_b32 s2, 0x418000
	s_nop 0
	v_addc_co_u32_e32 v109, vcc, 0, v3, vcc
	v_add_co_u32_e32 v118, vcc, s2, v2
	s_mov_b32 s2, 0x41a000
	s_nop 0
	v_addc_co_u32_e32 v119, vcc, 0, v3, vcc
	v_add_co_u32_e32 v122, vcc, s2, v2
	s_mov_b32 s2, 0x41c000
	s_nop 0
	v_addc_co_u32_e32 v123, vcc, 0, v3, vcc
	v_add_co_u32_e32 v126, vcc, s2, v2
	s_mov_b32 s2, 0x41e000
	s_nop 0
	v_addc_co_u32_e32 v127, vcc, 0, v3, vcc
	v_add_co_u32_e32 v128, vcc, s2, v2
	global_load_dwordx4 v[34:37], v[34:35], off sc0 nt
	s_nop 0
	global_load_dwordx4 v[38:41], v[38:39], off sc0 nt
	v_addc_co_u32_e32 v129, vcc, 0, v3, vcc
	global_load_dwordx4 v[58:61], v[50:51], off sc0 nt
	s_nop 0
	global_load_dwordx4 v[50:53], v[52:53], off sc0 nt
	s_nop 0
	global_load_dwordx4 v[62:65], v[62:63], off sc0 nt
	s_nop 0
	global_load_dwordx4 v[70:73], v[70:71], off sc0 nt
	s_nop 0
	global_load_dwordx4 v[90:93], v[74:75], off sc0 nt
	s_nop 0
	global_load_dwordx4 v[74:77], v[76:77], off sc0 nt
	s_nop 0
	global_load_dwordx4 v[94:97], v[94:95], off sc0 nt
	s_nop 0
	global_load_dwordx4 v[98:101], v[98:99], off sc0 nt
	s_nop 0
	global_load_dwordx4 v[114:117], v[106:107], off sc0 nt
	s_nop 0
	global_load_dwordx4 v[106:109], v[108:109], off sc0 nt
	s_nop 0
	global_load_dwordx4 v[118:121], v[118:119], off sc0 nt
	s_nop 0
	global_load_dwordx4 v[122:125], v[122:123], off sc0 nt
	s_nop 0
	global_load_dwordx4 v[130:133], v[126:127], off sc0 nt
	s_nop 0
	global_load_dwordx4 v[126:129], v[128:129], off sc0 nt
	v_add_u32_e32 v160, 0, v4
	v_lshl_add_u64 v[134:135], s[6:7], 0, v[4:5]
	s_mov_b64 s[2:3], 0x60000000
	v_lshl_add_u64 v[168:169], v[134:135], 0, s[2:3]
	v_mad_u64_u32 v[154:155], s[2:3], v136, s1, v[160:161]
	ds_read_b128 v[134:137], v154
	v_lshl_add_u64 v[150:151], v[168:169], 0, v[138:139]
	v_mad_u64_u32 v[156:157], s[2:3], v140, s1, v[160:161]
	v_mad_u64_u32 v[158:159], s[2:3], v144, s1, v[160:161]
	v_mad_u64_u32 v[162:163], s[2:3], v148, s1, v[160:161]
	ds_read_b128 v[138:141], v156
	s_waitcnt lgkmcnt(1)
	global_store_dwordx4 v[150:151], v[134:137], off nt
	v_lshl_add_u64 v[152:153], v[168:169], 0, v[142:143]
	ds_read_b128 v[134:137], v158
	ds_read_b128 v[142:145], v162
	v_lshl_add_u64 v[160:161], v[168:169], 0, v[146:147]
	v_lshl_add_u64 v[164:165], v[168:169], 0, v[164:165]
	s_waitcnt lgkmcnt(2)
	global_store_dwordx4 v[152:153], v[138:141], off nt
	s_waitcnt lgkmcnt(1)
	global_store_dwordx4 v[160:161], v[134:137], off nt
	s_waitcnt lgkmcnt(0)
	global_store_dwordx4 v[164:165], v[142:145], off nt
	s_waitcnt vmcnt(35)
	v_mul_f32_e32 v4, 0x43800000, v6
	s_waitcnt vmcnt(34)
	v_mul_f32_e32 v6, 0x43800000, v10
	v_med3_f32 v4, v4, s0, v1
	v_med3_f32 v6, v6, s0, v1
	v_mov_b32_e32 v134, v5
	v_cvt_pk_fp8_f32 v134, v4, v6
	s_waitcnt vmcnt(33)
	v_mul_f32_e32 v10, 0x43800000, v18
	s_waitcnt vmcnt(32)
	v_mul_f32_e32 v4, 0x43800000, v14
	v_med3_f32 v6, v10, s0, v1
	v_med3_f32 v4, v4, s0, v1
	v_cvt_pk_fp8_f32 v134, v6, v4 op_sel:[0,0,1]
	s_waitcnt vmcnt(31)
	v_mul_f32_e32 v4, 0x43800000, v22
	s_waitcnt vmcnt(30)
	v_mul_f32_e32 v6, 0x43800000, v26
	v_med3_f32 v4, v4, s0, v1
	v_med3_f32 v6, v6, s0, v1
	v_mov_b32_e32 v135, v5
	v_cvt_pk_fp8_f32 v135, v4, v6
	s_waitcnt vmcnt(29)
	v_mul_f32_e32 v10, 0x43800000, v42
	s_waitcnt vmcnt(28)
	v_mul_f32_e32 v4, 0x43800000, v30
	v_med3_f32 v6, v10, s0, v1
	v_med3_f32 v4, v4, s0, v1
	v_cvt_pk_fp8_f32 v135, v6, v4 op_sel:[0,0,1]
	s_waitcnt vmcnt(27)
	v_mul_f32_e32 v4, 0x43800000, v46
	s_waitcnt vmcnt(26)
	v_mul_f32_e32 v6, 0x43800000, v54
	v_med3_f32 v4, v4, s0, v1
	v_med3_f32 v6, v6, s0, v1
	v_mov_b32_e32 v136, v5
	v_cvt_pk_fp8_f32 v136, v4, v6
	s_waitcnt vmcnt(25)
	v_mul_f32_e32 v10, 0x43800000, v78
	s_waitcnt vmcnt(24)
	v_mul_f32_e32 v4, 0x43800000, v66
	v_med3_f32 v6, v10, s0, v1
	v_med3_f32 v4, v4, s0, v1
	v_cvt_pk_fp8_f32 v136, v6, v4 op_sel:[0,0,1]
	s_waitcnt vmcnt(23)
	v_mul_f32_e32 v4, 0x43800000, v82
	s_waitcnt vmcnt(22)
	v_mul_f32_e32 v6, 0x43800000, v86
	v_med3_f32 v4, v4, s0, v1
	v_med3_f32 v6, v6, s0, v1
	v_mov_b32_e32 v137, v5
	v_cvt_pk_fp8_f32 v137, v4, v6
	s_waitcnt vmcnt(21)
	v_mul_f32_e32 v10, 0x43800000, v110
	s_waitcnt vmcnt(20)
	v_mul_f32_e32 v4, 0x43800000, v102
	v_med3_f32 v6, v10, s0, v1
	v_med3_f32 v4, v4, s0, v1
	v_cvt_pk_fp8_f32 v137, v6, v4 op_sel:[0,0,1]
	v_mul_f32_e32 v4, 0x43800000, v7
	v_mul_f32_e32 v6, 0x43800000, v11
	v_med3_f32 v4, v4, s0, v1
	v_med3_f32 v6, v6, s0, v1
	v_mov_b32_e32 v138, v5
	v_cvt_pk_fp8_f32 v138, v4, v6
	v_mul_f32_e32 v7, 0x43800000, v19
	v_mul_f32_e32 v4, 0x43800000, v15
	v_med3_f32 v6, v7, s0, v1
	v_med3_f32 v4, v4, s0, v1
	v_cvt_pk_fp8_f32 v138, v6, v4 op_sel:[0,0,1]
	v_mul_f32_e32 v4, 0x43800000, v23
	v_mul_f32_e32 v6, 0x43800000, v27
	v_med3_f32 v4, v4, s0, v1
	v_med3_f32 v6, v6, s0, v1
	v_mov_b32_e32 v139, v5
	v_cvt_pk_fp8_f32 v139, v4, v6
	v_mul_f32_e32 v7, 0x43800000, v43
	v_mul_f32_e32 v4, 0x43800000, v31
	v_med3_f32 v6, v7, s0, v1
	v_med3_f32 v4, v4, s0, v1
	v_cvt_pk_fp8_f32 v139, v6, v4 op_sel:[0,0,1]
	v_mul_f32_e32 v4, 0x43800000, v47
	v_mul_f32_e32 v6, 0x43800000, v55
	v_med3_f32 v4, v4, s0, v1
	v_med3_f32 v6, v6, s0, v1
	v_mov_b32_e32 v140, v5
	v_cvt_pk_fp8_f32 v140, v4, v6
	v_mul_f32_e32 v7, 0x43800000, v79
	v_mul_f32_e32 v4, 0x43800000, v67
	v_med3_f32 v6, v7, s0, v1
	v_med3_f32 v4, v4, s0, v1
	v_cvt_pk_fp8_f32 v140, v6, v4 op_sel:[0,0,1]
	v_mul_f32_e32 v4, 0x43800000, v83
	v_mul_f32_e32 v6, 0x43800000, v87
	v_med3_f32 v4, v4, s0, v1
	v_med3_f32 v6, v6, s0, v1
	v_mov_b32_e32 v141, v5
	v_cvt_pk_fp8_f32 v141, v4, v6
	v_mul_f32_e32 v7, 0x43800000, v111
	v_mul_f32_e32 v4, 0x43800000, v103
	v_med3_f32 v6, v7, s0, v1
	v_med3_f32 v4, v4, s0, v1
	v_cvt_pk_fp8_f32 v141, v6, v4 op_sel:[0,0,1]
	v_mul_f32_e32 v4, 0x43800000, v8
	v_mul_f32_e32 v6, 0x43800000, v12
	v_med3_f32 v4, v4, s0, v1
	v_med3_f32 v6, v6, s0, v1
	v_mov_b32_e32 v142, v5
	v_cvt_pk_fp8_f32 v142, v4, v6
	v_mul_f32_e32 v7, 0x43800000, v20
	v_mul_f32_e32 v4, 0x43800000, v16
	v_med3_f32 v6, v7, s0, v1
	v_med3_f32 v4, v4, s0, v1
	v_cvt_pk_fp8_f32 v142, v6, v4 op_sel:[0,0,1]
	v_mul_f32_e32 v4, 0x43800000, v24
	v_mul_f32_e32 v6, 0x43800000, v28
	v_med3_f32 v4, v4, s0, v1
	v_med3_f32 v6, v6, s0, v1
	v_mov_b32_e32 v143, v5
	v_cvt_pk_fp8_f32 v143, v4, v6
	v_mul_f32_e32 v7, 0x43800000, v44
	v_mul_f32_e32 v4, 0x43800000, v32
	v_med3_f32 v6, v7, s0, v1
	v_med3_f32 v4, v4, s0, v1
	v_cvt_pk_fp8_f32 v143, v6, v4 op_sel:[0,0,1]
	v_mul_f32_e32 v4, 0x43800000, v48
	v_mul_f32_e32 v6, 0x43800000, v56
	v_med3_f32 v4, v4, s0, v1
	v_med3_f32 v6, v6, s0, v1
	v_mov_b32_e32 v144, v5
	v_cvt_pk_fp8_f32 v144, v4, v6
	v_mul_f32_e32 v7, 0x43800000, v80
	v_mul_f32_e32 v4, 0x43800000, v68
	v_med3_f32 v6, v7, s0, v1
	v_med3_f32 v4, v4, s0, v1
	v_cvt_pk_fp8_f32 v144, v6, v4 op_sel:[0,0,1]
	v_mul_f32_e32 v4, 0x43800000, v84
	v_mul_f32_e32 v6, 0x43800000, v88
	v_med3_f32 v4, v4, s0, v1
	v_med3_f32 v6, v6, s0, v1
	v_mov_b32_e32 v145, v5
	v_cvt_pk_fp8_f32 v145, v4, v6
	v_mul_f32_e32 v7, 0x43800000, v112
	v_mul_f32_e32 v4, 0x43800000, v104
	v_med3_f32 v6, v7, s0, v1
	v_med3_f32 v4, v4, s0, v1
	v_cvt_pk_fp8_f32 v145, v6, v4 op_sel:[0,0,1]
	v_mul_f32_e32 v4, 0x43800000, v9
	v_mul_f32_e32 v6, 0x43800000, v13
	v_med3_f32 v4, v4, s0, v1
	v_med3_f32 v8, v6, s0, v1
	v_mov_b32_e32 v6, v5
	v_cvt_pk_fp8_f32 v6, v4, v8
	v_mul_f32_e32 v7, 0x43800000, v21
	v_mul_f32_e32 v4, 0x43800000, v17
	v_med3_f32 v7, v7, s0, v1
	v_med3_f32 v4, v4, s0, v1
	v_cvt_pk_fp8_f32 v6, v7, v4 op_sel:[0,0,1]
	v_mul_f32_e32 v4, 0x43800000, v25
	v_mul_f32_e32 v7, 0x43800000, v29
	v_med3_f32 v4, v4, s0, v1
	v_med3_f32 v9, v7, s0, v1
	v_mov_b32_e32 v7, v5
	v_cvt_pk_fp8_f32 v7, v4, v9
	v_mul_f32_e32 v8, 0x43800000, v45
	v_mul_f32_e32 v4, 0x43800000, v33
	v_med3_f32 v8, v8, s0, v1
	v_med3_f32 v4, v4, s0, v1
	v_cvt_pk_fp8_f32 v7, v8, v4 op_sel:[0,0,1]
	v_mul_f32_e32 v4, 0x43800000, v49
	v_mul_f32_e32 v8, 0x43800000, v57
	v_med3_f32 v4, v4, s0, v1
	v_med3_f32 v10, v8, s0, v1
	v_mov_b32_e32 v8, v5
	v_cvt_pk_fp8_f32 v8, v4, v10
	v_mul_f32_e32 v9, 0x43800000, v81
	v_mul_f32_e32 v4, 0x43800000, v69
	v_med3_f32 v9, v9, s0, v1
	v_med3_f32 v4, v4, s0, v1
	v_cvt_pk_fp8_f32 v8, v9, v4 op_sel:[0,0,1]
	v_mul_f32_e32 v4, 0x43800000, v85
	v_mul_f32_e32 v9, 0x43800000, v89
	v_med3_f32 v4, v4, s0, v1
	v_med3_f32 v11, v9, s0, v1
	v_mov_b32_e32 v9, v5
	v_cvt_pk_fp8_f32 v9, v4, v11
	v_mul_f32_e32 v10, 0x43800000, v113
	v_mul_f32_e32 v4, 0x43800000, v105
	v_med3_f32 v10, v10, s0, v1
	v_med3_f32 v4, v4, s0, v1
	v_cvt_pk_fp8_f32 v9, v10, v4 op_sel:[0,0,1]
	ds_write_b128 v166, v[134:137] offset:34816
	ds_write_b128 v166, v[138:141] offset:35088
	ds_write_b128 v166, v[142:145] offset:35360
	ds_write_b128 v166, v[6:9] offset:35632
	s_waitcnt lgkmcnt(0)
	s_barrier
	s_mov_b32 s1, 0x600000
	v_add_co_u32_e32 v6, vcc, s1, v2
	s_mov_b32 s1, 0x602000
	s_nop 0
	v_addc_co_u32_e32 v7, vcc, 0, v3, vcc
	v_add_co_u32_e32 v10, vcc, s1, v2
	s_mov_b32 s1, 0x604000
	s_nop 0
	v_addc_co_u32_e32 v11, vcc, 0, v3, vcc
	global_load_dwordx4 v[6:9], v[6:7], off sc0 nt
	s_nop 0
	global_load_dwordx4 v[14:17], v[10:11], off sc0 nt
	v_add_co_u32_e32 v10, vcc, s1, v2
	s_mov_b32 s1, 0x606000
	s_nop 0
	v_addc_co_u32_e32 v11, vcc, 0, v3, vcc
	v_add_co_u32_e32 v12, vcc, s1, v2
	s_mov_b32 s1, 0x608000
	s_nop 0
	v_addc_co_u32_e32 v13, vcc, 0, v3, vcc
	global_load_dwordx4 v[30:33], v[10:11], off sc0 nt
	global_load_dwordx4 v[22:25], v[12:13], off sc0 nt
	v_add_co_u32_e32 v10, vcc, s1, v2
	s_mov_b32 s1, 0x60a000
	s_nop 0
	v_addc_co_u32_e32 v11, vcc, 0, v3, vcc
	v_add_co_u32_e32 v12, vcc, s1, v2
	s_mov_b32 s1, 0x60c000
	s_nop 0
	v_addc_co_u32_e32 v13, vcc, 0, v3, vcc
	global_load_dwordx4 v[42:45], v[10:11], off sc0 nt
	global_load_dwordx4 v[46:49], v[12:13], off sc0 nt
	v_add_co_u32_e32 v10, vcc, s1, v2
	s_mov_b32 s1, 0x60e000
	s_nop 0
	v_addc_co_u32_e32 v11, vcc, 0, v3, vcc
	v_add_co_u32_e32 v12, vcc, s1, v2
	s_mov_b32 s1, 0x610000
	s_nop 0
	v_addc_co_u32_e32 v13, vcc, 0, v3, vcc
	global_load_dwordx4 v[66:69], v[10:11], off sc0 nt
	global_load_dwordx4 v[54:57], v[12:13], off sc0 nt
	v_add_co_u32_e32 v10, vcc, s1, v2
	s_mov_b32 s1, 0x612000
	s_nop 0
	v_addc_co_u32_e32 v11, vcc, 0, v3, vcc
	v_add_co_u32_e32 v12, vcc, s1, v2
	s_mov_b32 s1, 0x614000
	s_nop 0
	v_addc_co_u32_e32 v13, vcc, 0, v3, vcc
	global_load_dwordx4 v[78:81], v[10:11], off sc0 nt
	global_load_dwordx4 v[82:85], v[12:13], off sc0 nt
	v_add_co_u32_e32 v10, vcc, s1, v2
	s_mov_b32 s1, 0x616000
	s_nop 0
	v_addc_co_u32_e32 v11, vcc, 0, v3, vcc
	v_add_co_u32_e32 v12, vcc, s1, v2
	s_mov_b32 s1, 0x618000
	s_nop 0
	v_addc_co_u32_e32 v13, vcc, 0, v3, vcc
	global_load_dwordx4 v[110:113], v[10:11], off sc0 nt
	global_load_dwordx4 v[102:105], v[12:13], off sc0 nt
	v_add_co_u32_e32 v10, vcc, s1, v2
	s_mov_b32 s1, 0x61a000
	s_nop 0
	v_addc_co_u32_e32 v11, vcc, 0, v3, vcc
	v_add_co_u32_e32 v12, vcc, s1, v2
	s_mov_b32 s1, 0x61c000
	s_nop 0
	v_addc_co_u32_e32 v13, vcc, 0, v3, vcc
	global_load_dwordx4 v[134:137], v[10:11], off sc0 nt
	global_load_dwordx4 v[138:141], v[12:13], off sc0 nt
	v_add_co_u32_e32 v10, vcc, s1, v2
	s_mov_b32 s1, 0x61e000
	s_nop 0
	v_addc_co_u32_e32 v11, vcc, 0, v3, vcc
	v_add_co_u32_e32 v12, vcc, s1, v2
	s_nop 1
	v_addc_co_u32_e32 v13, vcc, 0, v3, vcc
	global_load_dwordx4 v[146:149], v[10:11], off sc0 nt
	global_load_dwordx4 v[142:145], v[12:13], off sc0 nt
	ds_read_b128 v[10:13], v154 offset:34816
	ds_read_b128 v[18:21], v156 offset:34816
	ds_read_b128 v[26:29], v158 offset:34816
	ds_read_b128 v[86:89], v162 offset:34816
	s_waitcnt lgkmcnt(3)
	global_store_dwordx4 v[150:151], v[10:13], off offset:256 nt
	s_waitcnt lgkmcnt(2)
	global_store_dwordx4 v[152:153], v[18:21], off offset:256 nt
	s_waitcnt lgkmcnt(1)
	global_store_dwordx4 v[160:161], v[26:29], off offset:256 nt
	s_waitcnt lgkmcnt(0)
	global_store_dwordx4 v[164:165], v[86:89], off offset:256 nt
	s_waitcnt vmcnt(39)
	v_mul_f32_e32 v4, 0x43800000, v34
	s_waitcnt vmcnt(38)
	v_mul_f32_e32 v10, 0x43800000, v38
	v_med3_f32 v4, v4, s0, v1
	v_med3_f32 v12, v10, s0, v1
	v_mov_b32_e32 v10, v5
	v_cvt_pk_fp8_f32 v10, v4, v12
	s_waitcnt vmcnt(37)
	v_mul_f32_e32 v11, 0x43800000, v58
	s_waitcnt vmcnt(36)
	v_mul_f32_e32 v4, 0x43800000, v50
	v_med3_f32 v11, v11, s0, v1
	v_med3_f32 v4, v4, s0, v1
	v_cvt_pk_fp8_f32 v10, v11, v4 op_sel:[0,0,1]
	s_waitcnt vmcnt(35)
	v_mul_f32_e32 v4, 0x43800000, v62
	s_waitcnt vmcnt(34)
	v_mul_f32_e32 v11, 0x43800000, v70
	v_med3_f32 v4, v4, s0, v1
	v_med3_f32 v13, v11, s0, v1
	v_mov_b32_e32 v11, v5
	v_cvt_pk_fp8_f32 v11, v4, v13
	s_waitcnt vmcnt(33)
	v_mul_f32_e32 v12, 0x43800000, v90
	s_waitcnt vmcnt(32)
	v_mul_f32_e32 v4, 0x43800000, v74
	v_med3_f32 v12, v12, s0, v1
	v_med3_f32 v4, v4, s0, v1
	v_cvt_pk_fp8_f32 v11, v12, v4 op_sel:[0,0,1]
	s_waitcnt vmcnt(31)
	v_mul_f32_e32 v4, 0x43800000, v94
	s_waitcnt vmcnt(30)
	v_mul_f32_e32 v12, 0x43800000, v98
	v_med3_f32 v4, v4, s0, v1
	v_med3_f32 v18, v12, s0, v1
	v_mov_b32_e32 v12, v5
	v_cvt_pk_fp8_f32 v12, v4, v18
	s_waitcnt vmcnt(29)
	v_mul_f32_e32 v13, 0x43800000, v114
	s_waitcnt vmcnt(28)
	v_mul_f32_e32 v4, 0x43800000, v106
	v_med3_f32 v13, v13, s0, v1
	v_med3_f32 v4, v4, s0, v1
	v_cvt_pk_fp8_f32 v12, v13, v4 op_sel:[0,0,1]
	s_waitcnt vmcnt(27)
	v_mul_f32_e32 v4, 0x43800000, v118
	s_waitcnt vmcnt(26)
	v_mul_f32_e32 v13, 0x43800000, v122
	v_med3_f32 v4, v4, s0, v1
	v_med3_f32 v19, v13, s0, v1
	v_mov_b32_e32 v13, v5
	v_cvt_pk_fp8_f32 v13, v4, v19
	s_waitcnt vmcnt(25)
	v_mul_f32_e32 v18, 0x43800000, v130
	s_waitcnt vmcnt(24)
	v_mul_f32_e32 v4, 0x43800000, v126
	v_med3_f32 v18, v18, s0, v1
	v_med3_f32 v4, v4, s0, v1
	v_cvt_pk_fp8_f32 v13, v18, v4 op_sel:[0,0,1]
	v_mul_f32_e32 v4, 0x43800000, v35
	v_mul_f32_e32 v18, 0x43800000, v39
	v_med3_f32 v4, v4, s0, v1
	v_med3_f32 v20, v18, s0, v1
	v_mov_b32_e32 v18, v5
	v_cvt_pk_fp8_f32 v18, v4, v20
	v_mul_f32_e32 v19, 0x43800000, v59
	v_mul_f32_e32 v4, 0x43800000, v51
	v_med3_f32 v19, v19, s0, v1
	v_med3_f32 v4, v4, s0, v1
	v_cvt_pk_fp8_f32 v18, v19, v4 op_sel:[0,0,1]
	v_mul_f32_e32 v4, 0x43800000, v63
	v_mul_f32_e32 v19, 0x43800000, v71
	v_med3_f32 v4, v4, s0, v1
	v_med3_f32 v21, v19, s0, v1
	v_mov_b32_e32 v19, v5
	v_cvt_pk_fp8_f32 v19, v4, v21
	v_mul_f32_e32 v20, 0x43800000, v91
	v_mul_f32_e32 v4, 0x43800000, v75
	v_med3_f32 v20, v20, s0, v1
	v_med3_f32 v4, v4, s0, v1
	v_cvt_pk_fp8_f32 v19, v20, v4 op_sel:[0,0,1]
	v_mul_f32_e32 v4, 0x43800000, v95
	v_mul_f32_e32 v20, 0x43800000, v99
	v_med3_f32 v4, v4, s0, v1
	v_med3_f32 v26, v20, s0, v1
	v_mov_b32_e32 v20, v5
	v_cvt_pk_fp8_f32 v20, v4, v26
	v_mul_f32_e32 v21, 0x43800000, v115
	v_mul_f32_e32 v4, 0x43800000, v107
	v_med3_f32 v21, v21, s0, v1
	v_med3_f32 v4, v4, s0, v1
	v_cvt_pk_fp8_f32 v20, v21, v4 op_sel:[0,0,1]
	v_mul_f32_e32 v4, 0x43800000, v119
	v_mul_f32_e32 v21, 0x43800000, v123
	v_med3_f32 v4, v4, s0, v1
	v_med3_f32 v27, v21, s0, v1
	v_mov_b32_e32 v21, v5
	v_cvt_pk_fp8_f32 v21, v4, v27
	v_mul_f32_e32 v26, 0x43800000, v131
	v_mul_f32_e32 v4, 0x43800000, v127
	v_med3_f32 v26, v26, s0, v1
	v_med3_f32 v4, v4, s0, v1
	v_cvt_pk_fp8_f32 v21, v26, v4 op_sel:[0,0,1]
	v_mul_f32_e32 v4, 0x43800000, v36
	v_mul_f32_e32 v26, 0x43800000, v40
	v_med3_f32 v4, v4, s0, v1
	v_med3_f32 v28, v26, s0, v1
	v_mov_b32_e32 v26, v5
	v_cvt_pk_fp8_f32 v26, v4, v28
	v_mul_f32_e32 v27, 0x43800000, v60
	v_mul_f32_e32 v4, 0x43800000, v52
	v_med3_f32 v27, v27, s0, v1
	v_med3_f32 v4, v4, s0, v1
	v_cvt_pk_fp8_f32 v26, v27, v4 op_sel:[0,0,1]
	v_mul_f32_e32 v4, 0x43800000, v64
	v_mul_f32_e32 v27, 0x43800000, v72
	v_med3_f32 v4, v4, s0, v1
	v_med3_f32 v29, v27, s0, v1
	v_mov_b32_e32 v27, v5
	v_cvt_pk_fp8_f32 v27, v4, v29
	v_mul_f32_e32 v28, 0x43800000, v92
	v_mul_f32_e32 v4, 0x43800000, v76
	v_med3_f32 v28, v28, s0, v1
	v_med3_f32 v4, v4, s0, v1
	v_cvt_pk_fp8_f32 v27, v28, v4 op_sel:[0,0,1]
	v_mul_f32_e32 v4, 0x43800000, v96
	v_mul_f32_e32 v28, 0x43800000, v100
	v_med3_f32 v4, v4, s0, v1
	v_med3_f32 v34, v28, s0, v1
	v_mov_b32_e32 v28, v5
	v_cvt_pk_fp8_f32 v28, v4, v34
	v_mul_f32_e32 v29, 0x43800000, v116
	v_mul_f32_e32 v4, 0x43800000, v108
	v_med3_f32 v29, v29, s0, v1
	v_med3_f32 v4, v4, s0, v1
	v_cvt_pk_fp8_f32 v28, v29, v4 op_sel:[0,0,1]
	v_mul_f32_e32 v4, 0x43800000, v120
	v_mul_f32_e32 v29, 0x43800000, v124
	v_med3_f32 v4, v4, s0, v1
	v_med3_f32 v35, v29, s0, v1
	v_mov_b32_e32 v29, v5
	v_cvt_pk_fp8_f32 v29, v4, v35
	v_mul_f32_e32 v34, 0x43800000, v132
	v_mul_f32_e32 v4, 0x43800000, v128
	v_med3_f32 v34, v34, s0, v1
	v_med3_f32 v4, v4, s0, v1
	v_cvt_pk_fp8_f32 v29, v34, v4 op_sel:[0,0,1]
	v_mul_f32_e32 v4, 0x43800000, v37
	v_mul_f32_e32 v34, 0x43800000, v41
	v_med3_f32 v4, v4, s0, v1
	v_med3_f32 v36, v34, s0, v1
	v_mov_b32_e32 v34, v5
	v_cvt_pk_fp8_f32 v34, v4, v36
	v_mul_f32_e32 v35, 0x43800000, v61
	v_mul_f32_e32 v4, 0x43800000, v53
	v_med3_f32 v35, v35, s0, v1
	v_med3_f32 v4, v4, s0, v1
	v_cvt_pk_fp8_f32 v34, v35, v4 op_sel:[0,0,1]
	v_mul_f32_e32 v4, 0x43800000, v65
	v_mul_f32_e32 v35, 0x43800000, v73
	v_med3_f32 v4, v4, s0, v1
	v_med3_f32 v37, v35, s0, v1
	v_mov_b32_e32 v35, v5
	v_cvt_pk_fp8_f32 v35, v4, v37
	v_mul_f32_e32 v36, 0x43800000, v93
	v_mul_f32_e32 v4, 0x43800000, v77
	v_med3_f32 v36, v36, s0, v1
	v_med3_f32 v4, v4, s0, v1
	v_cvt_pk_fp8_f32 v35, v36, v4 op_sel:[0,0,1]
	v_mul_f32_e32 v4, 0x43800000, v97
	v_mul_f32_e32 v36, 0x43800000, v101
	v_med3_f32 v4, v4, s0, v1
	v_med3_f32 v38, v36, s0, v1
	v_mov_b32_e32 v36, v5
	v_cvt_pk_fp8_f32 v36, v4, v38
	v_mul_f32_e32 v37, 0x43800000, v117
	v_mul_f32_e32 v4, 0x43800000, v109
	v_med3_f32 v37, v37, s0, v1
	v_med3_f32 v4, v4, s0, v1
	v_cvt_pk_fp8_f32 v36, v37, v4 op_sel:[0,0,1]
	v_mul_f32_e32 v4, 0x43800000, v121
	v_mul_f32_e32 v37, 0x43800000, v125
	v_med3_f32 v4, v4, s0, v1
	v_med3_f32 v39, v37, s0, v1
	v_mov_b32_e32 v37, v5
	v_cvt_pk_fp8_f32 v37, v4, v39
	v_mul_f32_e32 v38, 0x43800000, v133
	v_mul_f32_e32 v4, 0x43800000, v129
	v_med3_f32 v38, v38, s0, v1
	v_med3_f32 v4, v4, s0, v1
	v_cvt_pk_fp8_f32 v37, v38, v4 op_sel:[0,0,1]
	ds_write_b128 v166, v[10:13]
	ds_write_b128 v166, v[18:21] offset:272
	ds_write_b128 v166, v[26:29] offset:544
	ds_write_b128 v166, v[34:37] offset:816
	s_waitcnt lgkmcnt(0)
	s_barrier
	s_mov_b32 s1, 0x800000
	v_add_co_u32_e32 v10, vcc, s1, v2
	s_mov_b32 s1, 0x802000
	s_nop 0
	v_addc_co_u32_e32 v11, vcc, 0, v3, vcc
	v_add_co_u32_e32 v18, vcc, s1, v2
	s_mov_b32 s1, 0x804000
	s_nop 0
	v_addc_co_u32_e32 v19, vcc, 0, v3, vcc
	v_add_co_u32_e32 v38, vcc, s1, v2
	s_mov_b32 s1, 0x806000
	s_nop 0
	v_addc_co_u32_e32 v39, vcc, 0, v3, vcc
	v_add_co_u32_e32 v40, vcc, s1, v2
	s_mov_b32 s1, 0x808000
	s_nop 0
	v_addc_co_u32_e32 v41, vcc, 0, v3, vcc
	v_add_co_u32_e32 v58, vcc, s1, v2
	s_mov_b32 s1, 0x80a000
	s_nop 0
	v_addc_co_u32_e32 v59, vcc, 0, v3, vcc
	v_add_co_u32_e32 v60, vcc, s1, v2
	s_mov_b32 s1, 0x80c000
	s_nop 0
	v_addc_co_u32_e32 v61, vcc, 0, v3, vcc
	v_add_co_u32_e32 v70, vcc, s1, v2
	s_mov_b32 s1, 0x80e000
	s_nop 0
	v_addc_co_u32_e32 v71, vcc, 0, v3, vcc
	v_add_co_u32_e32 v72, vcc, s1, v2
	s_mov_b32 s1, 0x810000
	s_nop 0
	v_addc_co_u32_e32 v73, vcc, 0, v3, vcc
	v_add_co_u32_e32 v74, vcc, s1, v2
	s_mov_b32 s1, 0x812000
	s_nop 0
	v_addc_co_u32_e32 v75, vcc, 0, v3, vcc
	v_add_co_u32_e32 v76, vcc, s1, v2
	s_mov_b32 s1, 0x814000
	s_nop 0
	v_addc_co_u32_e32 v77, vcc, 0, v3, vcc
	global_load_dwordx4 v[10:13], v[10:11], off sc0 nt
	s_nop 0
	global_load_dwordx4 v[18:21], v[18:19], off sc0 nt
	s_nop 0
	global_load_dwordx4 v[34:37], v[38:39], off sc0 nt
	global_load_dwordx4 v[26:29], v[40:41], off sc0 nt
	s_nop 0
	global_load_dwordx4 v[38:41], v[58:59], off sc0 nt
	global_load_dwordx4 v[50:53], v[60:61], off sc0 nt
	global_load_dwordx4 v[62:65], v[70:71], off sc0 nt
	s_nop 0
	global_load_dwordx4 v[58:61], v[72:73], off sc0 nt
	s_nop 0
	global_load_dwordx4 v[70:73], v[74:75], off sc0 nt
	global_load_dwordx4 v[86:89], v[76:77], off sc0 nt
	v_add_co_u32_e32 v74, vcc, s1, v2
	s_mov_b32 s1, 0x816000
	s_nop 0
	v_addc_co_u32_e32 v75, vcc, 0, v3, vcc
	v_add_co_u32_e32 v76, vcc, s1, v2
	s_mov_b32 s1, 0x818000
	s_nop 0
	v_addc_co_u32_e32 v77, vcc, 0, v3, vcc
	global_load_dwordx4 v[98:101], v[74:75], off sc0 nt
	global_load_dwordx4 v[90:93], v[76:77], off sc0 nt
	v_add_co_u32_e32 v74, vcc, s1, v2
	s_mov_b32 s1, 0x81a000
	s_nop 0
	v_addc_co_u32_e32 v75, vcc, 0, v3, vcc
	v_add_co_u32_e32 v76, vcc, s1, v2
	s_mov_b32 s1, 0x81c000
	s_nop 0
	v_addc_co_u32_e32 v77, vcc, 0, v3, vcc
	global_load_dwordx4 v[106:109], v[74:75], off sc0 nt
	global_load_dwordx4 v[114:117], v[76:77], off sc0 nt
	v_add_co_u32_e32 v74, vcc, s1, v2
	s_mov_b32 s1, 0x81e000
	s_nop 0
	v_addc_co_u32_e32 v75, vcc, 0, v3, vcc
	v_add_co_u32_e32 v76, vcc, s1, v2
	s_nop 1
	v_addc_co_u32_e32 v77, vcc, 0, v3, vcc
	global_load_dwordx4 v[130:133], v[74:75], off sc0 nt
	global_load_dwordx4 v[122:125], v[76:77], off sc0 nt
	ds_read_b128 v[74:77], v154
	ds_read_b128 v[94:97], v156
	ds_read_b128 v[118:121], v158
	ds_read_b128 v[126:129], v162
	s_waitcnt lgkmcnt(3)
	global_store_dwordx4 v[150:151], v[74:77], off offset:512 nt
	s_waitcnt lgkmcnt(2)
	global_store_dwordx4 v[152:153], v[94:97], off offset:512 nt
	s_waitcnt lgkmcnt(1)
	global_store_dwordx4 v[160:161], v[118:121], off offset:512 nt
	s_waitcnt lgkmcnt(0)
	global_store_dwordx4 v[164:165], v[126:129], off offset:512 nt
	s_waitcnt vmcnt(39)
	v_mul_f32_e32 v4, 0x43800000, v6
	s_waitcnt vmcnt(38)
	v_mul_f32_e32 v6, 0x43800000, v14
	v_med3_f32 v4, v4, s0, v1
	v_med3_f32 v6, v6, s0, v1
	v_mov_b32_e32 v74, v5
	v_cvt_pk_fp8_f32 v74, v4, v6
	s_waitcnt vmcnt(37)
	v_mul_f32_e32 v14, 0x43800000, v30
	s_waitcnt vmcnt(36)
	v_mul_f32_e32 v4, 0x43800000, v22
	v_med3_f32 v6, v14, s0, v1
	v_med3_f32 v4, v4, s0, v1
	v_cvt_pk_fp8_f32 v74, v6, v4 op_sel:[0,0,1]
	s_waitcnt vmcnt(35)
	v_mul_f32_e32 v4, 0x43800000, v42
	s_waitcnt vmcnt(34)
	v_mul_f32_e32 v6, 0x43800000, v46
	v_med3_f32 v4, v4, s0, v1
	v_med3_f32 v6, v6, s0, v1
	v_mov_b32_e32 v75, v5
	v_cvt_pk_fp8_f32 v75, v4, v6
	s_waitcnt vmcnt(33)
	v_mul_f32_e32 v14, 0x43800000, v66
	s_waitcnt vmcnt(32)
	v_mul_f32_e32 v4, 0x43800000, v54
	v_med3_f32 v6, v14, s0, v1
	v_med3_f32 v4, v4, s0, v1
	v_cvt_pk_fp8_f32 v75, v6, v4 op_sel:[0,0,1]
	s_waitcnt vmcnt(31)
	v_mul_f32_e32 v4, 0x43800000, v78
	s_waitcnt vmcnt(30)
	v_mul_f32_e32 v6, 0x43800000, v82
	v_med3_f32 v4, v4, s0, v1
	v_med3_f32 v6, v6, s0, v1
	v_mov_b32_e32 v76, v5
	v_cvt_pk_fp8_f32 v76, v4, v6
	s_waitcnt vmcnt(29)
	v_mul_f32_e32 v14, 0x43800000, v110
	s_waitcnt vmcnt(28)
	v_mul_f32_e32 v4, 0x43800000, v102
	v_med3_f32 v6, v14, s0, v1
	v_med3_f32 v4, v4, s0, v1
	v_cvt_pk_fp8_f32 v76, v6, v4 op_sel:[0,0,1]
	s_waitcnt vmcnt(27)
	v_mul_f32_e32 v4, 0x43800000, v134
	s_waitcnt vmcnt(26)
	v_mul_f32_e32 v6, 0x43800000, v138
	v_med3_f32 v4, v4, s0, v1
	v_med3_f32 v6, v6, s0, v1
	v_mov_b32_e32 v77, v5
	v_cvt_pk_fp8_f32 v77, v4, v6
	s_waitcnt vmcnt(25)
	v_mul_f32_e32 v14, 0x43800000, v146
	s_waitcnt vmcnt(24)
	v_mul_f32_e32 v4, 0x43800000, v142
	v_med3_f32 v6, v14, s0, v1
	v_med3_f32 v4, v4, s0, v1
	v_cvt_pk_fp8_f32 v77, v6, v4 op_sel:[0,0,1]
	v_mul_f32_e32 v4, 0x43800000, v7
	v_mul_f32_e32 v6, 0x43800000, v15
	v_med3_f32 v4, v4, s0, v1
	v_med3_f32 v6, v6, s0, v1
	v_mov_b32_e32 v94, v5
	v_cvt_pk_fp8_f32 v94, v4, v6
	v_mul_f32_e32 v7, 0x43800000, v31
	v_mul_f32_e32 v4, 0x43800000, v23
	v_med3_f32 v6, v7, s0, v1
	v_med3_f32 v4, v4, s0, v1
	v_cvt_pk_fp8_f32 v94, v6, v4 op_sel:[0,0,1]
	v_mul_f32_e32 v4, 0x43800000, v43
	v_mul_f32_e32 v6, 0x43800000, v47
	v_med3_f32 v4, v4, s0, v1
	v_med3_f32 v6, v6, s0, v1
	v_mov_b32_e32 v95, v5
	v_cvt_pk_fp8_f32 v95, v4, v6
	v_mul_f32_e32 v7, 0x43800000, v67
	v_mul_f32_e32 v4, 0x43800000, v55
	v_med3_f32 v6, v7, s0, v1
	v_med3_f32 v4, v4, s0, v1
	v_cvt_pk_fp8_f32 v95, v6, v4 op_sel:[0,0,1]
	v_mul_f32_e32 v4, 0x43800000, v79
	v_mul_f32_e32 v6, 0x43800000, v83
	v_med3_f32 v4, v4, s0, v1
	v_med3_f32 v6, v6, s0, v1
	v_mov_b32_e32 v96, v5
	v_cvt_pk_fp8_f32 v96, v4, v6
	v_mul_f32_e32 v7, 0x43800000, v111
	v_mul_f32_e32 v4, 0x43800000, v103
	v_med3_f32 v6, v7, s0, v1
	v_med3_f32 v4, v4, s0, v1
	v_cvt_pk_fp8_f32 v96, v6, v4 op_sel:[0,0,1]
	v_mul_f32_e32 v4, 0x43800000, v135
	v_mul_f32_e32 v6, 0x43800000, v139
	v_med3_f32 v4, v4, s0, v1
	v_med3_f32 v6, v6, s0, v1
	v_mov_b32_e32 v97, v5
	v_cvt_pk_fp8_f32 v97, v4, v6
	v_mul_f32_e32 v7, 0x43800000, v147
	v_mul_f32_e32 v4, 0x43800000, v143
	v_med3_f32 v6, v7, s0, v1
	v_med3_f32 v4, v4, s0, v1
	v_cvt_pk_fp8_f32 v97, v6, v4 op_sel:[0,0,1]
	v_mul_f32_e32 v4, 0x43800000, v8
	v_mul_f32_e32 v6, 0x43800000, v16
	v_med3_f32 v4, v4, s0, v1
	v_med3_f32 v6, v6, s0, v1
	v_mov_b32_e32 v118, v5
	v_cvt_pk_fp8_f32 v118, v4, v6
	v_mul_f32_e32 v7, 0x43800000, v32
	v_mul_f32_e32 v4, 0x43800000, v24
	v_med3_f32 v6, v7, s0, v1
	v_med3_f32 v4, v4, s0, v1
	v_cvt_pk_fp8_f32 v118, v6, v4 op_sel:[0,0,1]
	v_mul_f32_e32 v4, 0x43800000, v44
	v_mul_f32_e32 v6, 0x43800000, v48
	v_med3_f32 v4, v4, s0, v1
	v_med3_f32 v6, v6, s0, v1
	v_mov_b32_e32 v119, v5
	v_cvt_pk_fp8_f32 v119, v4, v6
	v_mul_f32_e32 v7, 0x43800000, v68
	v_mul_f32_e32 v4, 0x43800000, v56
	v_med3_f32 v6, v7, s0, v1
	v_med3_f32 v4, v4, s0, v1
	v_cvt_pk_fp8_f32 v119, v6, v4 op_sel:[0,0,1]
	v_mul_f32_e32 v4, 0x43800000, v80
	v_mul_f32_e32 v6, 0x43800000, v84
	v_med3_f32 v4, v4, s0, v1
	v_med3_f32 v6, v6, s0, v1
	v_mov_b32_e32 v120, v5
	v_cvt_pk_fp8_f32 v120, v4, v6
	v_mul_f32_e32 v7, 0x43800000, v112
	v_mul_f32_e32 v4, 0x43800000, v104
	v_med3_f32 v6, v7, s0, v1
	v_med3_f32 v4, v4, s0, v1
	v_cvt_pk_fp8_f32 v120, v6, v4 op_sel:[0,0,1]
	v_mul_f32_e32 v4, 0x43800000, v136
	v_mul_f32_e32 v6, 0x43800000, v140
	v_med3_f32 v4, v4, s0, v1
	v_med3_f32 v6, v6, s0, v1
	v_mov_b32_e32 v121, v5
	v_cvt_pk_fp8_f32 v121, v4, v6
	v_mul_f32_e32 v7, 0x43800000, v148
	v_mul_f32_e32 v4, 0x43800000, v144
	v_med3_f32 v6, v7, s0, v1
	v_med3_f32 v4, v4, s0, v1
	v_cvt_pk_fp8_f32 v121, v6, v4 op_sel:[0,0,1]
	v_mul_f32_e32 v4, 0x43800000, v9
	v_mul_f32_e32 v6, 0x43800000, v17
	v_med3_f32 v4, v4, s0, v1
	v_med3_f32 v8, v6, s0, v1
	v_mov_b32_e32 v6, v5
	v_cvt_pk_fp8_f32 v6, v4, v8
	v_mul_f32_e32 v7, 0x43800000, v33
	v_mul_f32_e32 v4, 0x43800000, v25
	v_med3_f32 v7, v7, s0, v1
	v_med3_f32 v4, v4, s0, v1
	v_cvt_pk_fp8_f32 v6, v7, v4 op_sel:[0,0,1]
	v_mul_f32_e32 v4, 0x43800000, v45
	v_mul_f32_e32 v7, 0x43800000, v49
	v_med3_f32 v4, v4, s0, v1
	v_med3_f32 v9, v7, s0, v1
	v_mov_b32_e32 v7, v5
	v_cvt_pk_fp8_f32 v7, v4, v9
	v_mul_f32_e32 v8, 0x43800000, v69
	v_mul_f32_e32 v4, 0x43800000, v57
	v_med3_f32 v8, v8, s0, v1
	v_med3_f32 v4, v4, s0, v1
	v_cvt_pk_fp8_f32 v7, v8, v4 op_sel:[0,0,1]
	v_mul_f32_e32 v4, 0x43800000, v81
	v_mul_f32_e32 v8, 0x43800000, v85
	v_med3_f32 v4, v4, s0, v1
	v_med3_f32 v14, v8, s0, v1
	v_mov_b32_e32 v8, v5
	v_cvt_pk_fp8_f32 v8, v4, v14
	v_mul_f32_e32 v9, 0x43800000, v113
	v_mul_f32_e32 v4, 0x43800000, v105
	v_med3_f32 v9, v9, s0, v1
	v_med3_f32 v4, v4, s0, v1
	v_cvt_pk_fp8_f32 v8, v9, v4 op_sel:[0,0,1]
	v_mul_f32_e32 v4, 0x43800000, v137
	v_mul_f32_e32 v9, 0x43800000, v141
	v_med3_f32 v4, v4, s0, v1
	v_med3_f32 v15, v9, s0, v1
	v_mov_b32_e32 v9, v5
	v_cvt_pk_fp8_f32 v9, v4, v15
	v_mul_f32_e32 v14, 0x43800000, v149
	v_mul_f32_e32 v4, 0x43800000, v145
	v_med3_f32 v14, v14, s0, v1
	v_med3_f32 v4, v4, s0, v1
	v_cvt_pk_fp8_f32 v9, v14, v4 op_sel:[0,0,1]
	ds_write_b128 v166, v[74:77] offset:34816
	ds_write_b128 v166, v[94:97] offset:35088
	ds_write_b128 v166, v[118:121] offset:35360
	ds_write_b128 v166, v[6:9] offset:35632
	s_waitcnt lgkmcnt(0)
	s_barrier
	s_mov_b32 s1, 0xa00000
	v_add_co_u32_e32 v6, vcc, s1, v2
	s_mov_b32 s1, 0xa02000
	s_nop 0
	v_addc_co_u32_e32 v7, vcc, 0, v3, vcc
	v_add_co_u32_e32 v14, vcc, s1, v2
	s_mov_b32 s1, 0xa04000
	s_nop 0
	v_addc_co_u32_e32 v15, vcc, 0, v3, vcc
	v_add_co_u32_e32 v42, vcc, s1, v2
	s_mov_b32 s1, 0xa06000
	s_nop 0
	v_addc_co_u32_e32 v43, vcc, 0, v3, vcc
	v_add_co_u32_e32 v44, vcc, s1, v2
	s_mov_b32 s1, 0xa08000
	s_nop 0
	v_addc_co_u32_e32 v45, vcc, 0, v3, vcc
	v_add_co_u32_e32 v54, vcc, s1, v2
	s_mov_b32 s1, 0xa0a000
	s_nop 0
	v_addc_co_u32_e32 v55, vcc, 0, v3, vcc
	v_add_co_u32_e32 v56, vcc, s1, v2
	s_mov_b32 s1, 0xa0c000
	s_nop 0
	v_addc_co_u32_e32 v57, vcc, 0, v3, vcc
	v_add_co_u32_e32 v74, vcc, s1, v2
	s_mov_b32 s1, 0xa0e000
	s_nop 0
	v_addc_co_u32_e32 v75, vcc, 0, v3, vcc
	v_add_co_u32_e32 v76, vcc, s1, v2
	s_mov_b32 s1, 0xa10000
	s_nop 0
	v_addc_co_u32_e32 v77, vcc, 0, v3, vcc
	v_add_co_u32_e32 v82, vcc, s1, v2
	s_mov_b32 s1, 0xa12000
	s_nop 0
	v_addc_co_u32_e32 v83, vcc, 0, v3, vcc
	v_add_co_u32_e32 v84, vcc, s1, v2
	s_mov_b32 s1, 0xa14000
	s_nop 0
	v_addc_co_u32_e32 v85, vcc, 0, v3, vcc
	global_load_dwordx4 v[6:9], v[6:7], off sc0 nt
	s_nop 0
	global_load_dwordx4 v[14:17], v[14:15], off sc0 nt
	s_nop 0
	global_load_dwordx4 v[30:33], v[42:43], off sc0 nt
	global_load_dwordx4 v[22:25], v[44:45], off sc0 nt
	s_nop 0
	global_load_dwordx4 v[42:45], v[54:55], off sc0 nt
	global_load_dwordx4 v[46:49], v[56:57], off sc0 nt
	global_load_dwordx4 v[66:69], v[74:75], off sc0 nt
	s_nop 0
	global_load_dwordx4 v[54:57], v[76:77], off sc0 nt
	s_nop 0
	global_load_dwordx4 v[74:77], v[82:83], off sc0 nt
	global_load_dwordx4 v[78:81], v[84:85], off sc0 nt
	v_add_co_u32_e32 v82, vcc, s1, v2
	s_mov_b32 s1, 0xa16000
	s_nop 0
	v_addc_co_u32_e32 v83, vcc, 0, v3, vcc
	v_add_co_u32_e32 v84, vcc, s1, v2
	s_mov_b32 s1, 0xa18000
	s_nop 0
	v_addc_co_u32_e32 v85, vcc, 0, v3, vcc
	global_load_dwordx4 v[102:105], v[82:83], off sc0 nt
	global_load_dwordx4 v[94:97], v[84:85], off sc0 nt
	v_add_co_u32_e32 v82, vcc, s1, v2
	s_mov_b32 s1, 0xa1a000
	s_nop 0
	v_addc_co_u32_e32 v83, vcc, 0, v3, vcc
	v_add_co_u32_e32 v84, vcc, s1, v2
	s_mov_b32 s1, 0xa1c000
	s_nop 0
	v_addc_co_u32_e32 v85, vcc, 0, v3, vcc
	global_load_dwordx4 v[110:113], v[82:83], off sc0 nt
	global_load_dwordx4 v[118:121], v[84:85], off sc0 nt
	v_add_co_u32_e32 v82, vcc, s1, v2
	s_mov_b32 s1, 0xa1e000
	s_nop 0
	v_addc_co_u32_e32 v83, vcc, 0, v3, vcc
	v_add_co_u32_e32 v84, vcc, s1, v2
	s_nop 1
	v_addc_co_u32_e32 v85, vcc, 0, v3, vcc
	global_load_dwordx4 v[134:137], v[82:83], off sc0 nt
	global_load_dwordx4 v[126:129], v[84:85], off sc0 nt
	ds_read_b128 v[82:85], v154 offset:34816
	ds_read_b128 v[138:141], v156 offset:34816
	ds_read_b128 v[142:145], v158 offset:34816
	ds_read_b128 v[146:149], v162 offset:34816
	s_waitcnt lgkmcnt(3)
	global_store_dwordx4 v[150:151], v[82:85], off offset:768 nt
	s_waitcnt lgkmcnt(2)
	global_store_dwordx4 v[152:153], v[138:141], off offset:768 nt
	s_waitcnt lgkmcnt(1)
	global_store_dwordx4 v[160:161], v[142:145], off offset:768 nt
	s_waitcnt lgkmcnt(0)
	global_store_dwordx4 v[164:165], v[146:149], off offset:768 nt
	s_waitcnt vmcnt(39)
	v_mul_f32_e32 v4, 0x43800000, v10
	s_waitcnt vmcnt(38)
	v_mul_f32_e32 v10, 0x43800000, v18
	v_med3_f32 v4, v4, s0, v1
	v_med3_f32 v10, v10, s0, v1
	v_mov_b32_e32 v82, v5
	v_cvt_pk_fp8_f32 v82, v4, v10
	s_waitcnt vmcnt(37)
	v_mul_f32_e32 v18, 0x43800000, v34
	s_waitcnt vmcnt(36)
	v_mul_f32_e32 v4, 0x43800000, v26
	v_med3_f32 v10, v18, s0, v1
	v_med3_f32 v4, v4, s0, v1
	v_cvt_pk_fp8_f32 v82, v10, v4 op_sel:[0,0,1]
	s_waitcnt vmcnt(35)
	v_mul_f32_e32 v4, 0x43800000, v38
	s_waitcnt vmcnt(34)
	v_mul_f32_e32 v10, 0x43800000, v50
	v_med3_f32 v4, v4, s0, v1
	v_med3_f32 v10, v10, s0, v1
	v_mov_b32_e32 v83, v5
	v_cvt_pk_fp8_f32 v83, v4, v10
	s_waitcnt vmcnt(33)
	v_mul_f32_e32 v18, 0x43800000, v62
	s_waitcnt vmcnt(32)
	v_mul_f32_e32 v4, 0x43800000, v58
	v_med3_f32 v10, v18, s0, v1
	v_med3_f32 v4, v4, s0, v1
	v_cvt_pk_fp8_f32 v83, v10, v4 op_sel:[0,0,1]
	s_waitcnt vmcnt(31)
	v_mul_f32_e32 v4, 0x43800000, v70
	s_waitcnt vmcnt(30)
	v_mul_f32_e32 v10, 0x43800000, v86
	v_med3_f32 v4, v4, s0, v1
	v_med3_f32 v10, v10, s0, v1
	v_mov_b32_e32 v84, v5
	v_cvt_pk_fp8_f32 v84, v4, v10
	s_waitcnt vmcnt(29)
	v_mul_f32_e32 v18, 0x43800000, v98
	s_waitcnt vmcnt(28)
	v_mul_f32_e32 v4, 0x43800000, v90
	v_med3_f32 v10, v18, s0, v1
	v_med3_f32 v4, v4, s0, v1
	v_cvt_pk_fp8_f32 v84, v10, v4 op_sel:[0,0,1]
	s_waitcnt vmcnt(27)
	v_mul_f32_e32 v4, 0x43800000, v106
	s_waitcnt vmcnt(26)
	v_mul_f32_e32 v10, 0x43800000, v114
	v_med3_f32 v4, v4, s0, v1
	v_med3_f32 v10, v10, s0, v1
	v_mov_b32_e32 v85, v5
	v_cvt_pk_fp8_f32 v85, v4, v10
	s_waitcnt vmcnt(25)
	v_mul_f32_e32 v18, 0x43800000, v130
	s_waitcnt vmcnt(24)
	v_mul_f32_e32 v4, 0x43800000, v122
	v_med3_f32 v10, v18, s0, v1
	v_med3_f32 v4, v4, s0, v1
	v_cvt_pk_fp8_f32 v85, v10, v4 op_sel:[0,0,1]
	v_mul_f32_e32 v4, 0x43800000, v11
	v_mul_f32_e32 v10, 0x43800000, v19
	v_med3_f32 v4, v4, s0, v1
	v_med3_f32 v10, v10, s0, v1
	v_mov_b32_e32 v138, v5
	v_cvt_pk_fp8_f32 v138, v4, v10
	v_mul_f32_e32 v11, 0x43800000, v35
	v_mul_f32_e32 v4, 0x43800000, v27
	v_med3_f32 v10, v11, s0, v1
	v_med3_f32 v4, v4, s0, v1
	v_cvt_pk_fp8_f32 v138, v10, v4 op_sel:[0,0,1]
	v_mul_f32_e32 v4, 0x43800000, v39
	v_mul_f32_e32 v10, 0x43800000, v51
	v_med3_f32 v4, v4, s0, v1
	v_med3_f32 v10, v10, s0, v1
	v_mov_b32_e32 v139, v5
	v_cvt_pk_fp8_f32 v139, v4, v10
	v_mul_f32_e32 v11, 0x43800000, v63
	v_mul_f32_e32 v4, 0x43800000, v59
	v_med3_f32 v10, v11, s0, v1
	v_med3_f32 v4, v4, s0, v1
	v_cvt_pk_fp8_f32 v139, v10, v4 op_sel:[0,0,1]
	v_mul_f32_e32 v4, 0x43800000, v71
	v_mul_f32_e32 v10, 0x43800000, v87
	v_med3_f32 v4, v4, s0, v1
	v_med3_f32 v10, v10, s0, v1
	v_mov_b32_e32 v140, v5
	v_cvt_pk_fp8_f32 v140, v4, v10
	v_mul_f32_e32 v11, 0x43800000, v99
	v_mul_f32_e32 v4, 0x43800000, v91
	v_med3_f32 v10, v11, s0, v1
	v_med3_f32 v4, v4, s0, v1
	v_cvt_pk_fp8_f32 v140, v10, v4 op_sel:[0,0,1]
	v_mul_f32_e32 v4, 0x43800000, v107
	v_mul_f32_e32 v10, 0x43800000, v115
	v_med3_f32 v4, v4, s0, v1
	v_med3_f32 v10, v10, s0, v1
	v_mov_b32_e32 v141, v5
	v_cvt_pk_fp8_f32 v141, v4, v10
	v_mul_f32_e32 v11, 0x43800000, v131
	v_mul_f32_e32 v4, 0x43800000, v123
	v_med3_f32 v10, v11, s0, v1
	v_med3_f32 v4, v4, s0, v1
	v_cvt_pk_fp8_f32 v141, v10, v4 op_sel:[0,0,1]
	v_mul_f32_e32 v4, 0x43800000, v12
	v_mul_f32_e32 v10, 0x43800000, v20
	v_med3_f32 v4, v4, s0, v1
	v_med3_f32 v10, v10, s0, v1
	v_mov_b32_e32 v142, v5
	v_cvt_pk_fp8_f32 v142, v4, v10
	v_mul_f32_e32 v11, 0x43800000, v36
	v_mul_f32_e32 v4, 0x43800000, v28
	v_med3_f32 v10, v11, s0, v1
	v_med3_f32 v4, v4, s0, v1
	v_cvt_pk_fp8_f32 v142, v10, v4 op_sel:[0,0,1]
	v_mul_f32_e32 v4, 0x43800000, v40
	v_mul_f32_e32 v10, 0x43800000, v52
	v_med3_f32 v4, v4, s0, v1
	v_med3_f32 v10, v10, s0, v1
	v_mov_b32_e32 v143, v5
	v_cvt_pk_fp8_f32 v143, v4, v10
	v_mul_f32_e32 v11, 0x43800000, v64
	v_mul_f32_e32 v4, 0x43800000, v60
	v_med3_f32 v10, v11, s0, v1
	v_med3_f32 v4, v4, s0, v1
	v_cvt_pk_fp8_f32 v143, v10, v4 op_sel:[0,0,1]
	v_mul_f32_e32 v4, 0x43800000, v72
	v_mul_f32_e32 v10, 0x43800000, v88
	v_med3_f32 v4, v4, s0, v1
	v_med3_f32 v10, v10, s0, v1
	v_mov_b32_e32 v144, v5
	v_cvt_pk_fp8_f32 v144, v4, v10
	v_mul_f32_e32 v11, 0x43800000, v100
	v_mul_f32_e32 v4, 0x43800000, v92
	v_med3_f32 v10, v11, s0, v1
	v_med3_f32 v4, v4, s0, v1
	v_cvt_pk_fp8_f32 v144, v10, v4 op_sel:[0,0,1]
	v_mul_f32_e32 v4, 0x43800000, v108
	v_mul_f32_e32 v10, 0x43800000, v116
	v_med3_f32 v4, v4, s0, v1
	v_med3_f32 v10, v10, s0, v1
	v_mov_b32_e32 v145, v5
	v_cvt_pk_fp8_f32 v145, v4, v10
	v_mul_f32_e32 v11, 0x43800000, v132
	v_mul_f32_e32 v4, 0x43800000, v124
	v_med3_f32 v10, v11, s0, v1
	v_med3_f32 v4, v4, s0, v1
	v_cvt_pk_fp8_f32 v145, v10, v4 op_sel:[0,0,1]
	v_mul_f32_e32 v4, 0x43800000, v13
	v_mul_f32_e32 v10, 0x43800000, v21
	v_med3_f32 v4, v4, s0, v1
	v_med3_f32 v12, v10, s0, v1
	v_mov_b32_e32 v10, v5
	v_cvt_pk_fp8_f32 v10, v4, v12
	v_mul_f32_e32 v11, 0x43800000, v37
	v_mul_f32_e32 v4, 0x43800000, v29
	v_med3_f32 v11, v11, s0, v1
	v_med3_f32 v4, v4, s0, v1
	v_cvt_pk_fp8_f32 v10, v11, v4 op_sel:[0,0,1]
	v_mul_f32_e32 v4, 0x43800000, v41
	v_mul_f32_e32 v11, 0x43800000, v53
	v_med3_f32 v4, v4, s0, v1
	v_med3_f32 v13, v11, s0, v1
	v_mov_b32_e32 v11, v5
	v_cvt_pk_fp8_f32 v11, v4, v13
	v_mul_f32_e32 v12, 0x43800000, v65
	v_mul_f32_e32 v4, 0x43800000, v61
	v_med3_f32 v12, v12, s0, v1
	v_med3_f32 v4, v4, s0, v1
	v_cvt_pk_fp8_f32 v11, v12, v4 op_sel:[0,0,1]
	v_mul_f32_e32 v4, 0x43800000, v73
	v_mul_f32_e32 v12, 0x43800000, v89
	v_med3_f32 v4, v4, s0, v1
	v_med3_f32 v18, v12, s0, v1
	v_mov_b32_e32 v12, v5
	v_cvt_pk_fp8_f32 v12, v4, v18
	v_mul_f32_e32 v13, 0x43800000, v101
	v_mul_f32_e32 v4, 0x43800000, v93
	v_med3_f32 v13, v13, s0, v1
	v_med3_f32 v4, v4, s0, v1
	v_cvt_pk_fp8_f32 v12, v13, v4 op_sel:[0,0,1]
	v_mul_f32_e32 v4, 0x43800000, v109
	v_mul_f32_e32 v13, 0x43800000, v117
	v_med3_f32 v4, v4, s0, v1
	v_med3_f32 v19, v13, s0, v1
	v_mov_b32_e32 v13, v5
	v_cvt_pk_fp8_f32 v13, v4, v19
	v_mul_f32_e32 v18, 0x43800000, v133
	v_mul_f32_e32 v4, 0x43800000, v125
	v_med3_f32 v18, v18, s0, v1
	v_med3_f32 v4, v4, s0, v1
	v_cvt_pk_fp8_f32 v13, v18, v4 op_sel:[0,0,1]
	ds_write_b128 v166, v[82:85]
	ds_write_b128 v166, v[138:141] offset:272
	ds_write_b128 v166, v[142:145] offset:544
	ds_write_b128 v166, v[10:13] offset:816
	s_waitcnt lgkmcnt(0)
	s_barrier
	s_mov_b32 s1, 0xc00000
	v_add_co_u32_e32 v10, vcc, s1, v2
	s_mov_b32 s1, 0xc02000
	s_nop 0
	v_addc_co_u32_e32 v11, vcc, 0, v3, vcc
	v_add_co_u32_e32 v18, vcc, s1, v2
	s_mov_b32 s1, 0xc04000
	s_nop 0
	v_addc_co_u32_e32 v19, vcc, 0, v3, vcc
	v_add_co_u32_e32 v38, vcc, s1, v2
	s_mov_b32 s1, 0xc06000
	s_nop 0
	v_addc_co_u32_e32 v39, vcc, 0, v3, vcc
	v_add_co_u32_e32 v40, vcc, s1, v2
	s_mov_b32 s1, 0xc08000
	s_nop 0
	v_addc_co_u32_e32 v41, vcc, 0, v3, vcc
	v_add_co_u32_e32 v58, vcc, s1, v2
	s_mov_b32 s1, 0xc0a000
	s_nop 0
	v_addc_co_u32_e32 v59, vcc, 0, v3, vcc
	v_add_co_u32_e32 v60, vcc, s1, v2
	s_mov_b32 s1, 0xc0c000
	s_nop 0
	v_addc_co_u32_e32 v61, vcc, 0, v3, vcc
	v_add_co_u32_e32 v70, vcc, s1, v2
	s_mov_b32 s1, 0xc0e000
	s_nop 0
	v_addc_co_u32_e32 v71, vcc, 0, v3, vcc
	v_add_co_u32_e32 v72, vcc, s1, v2
	s_mov_b32 s1, 0xc10000
	s_nop 0
	v_addc_co_u32_e32 v73, vcc, 0, v3, vcc
	v_add_co_u32_e32 v86, vcc, s1, v2
	s_mov_b32 s1, 0xc12000
	s_nop 0
	v_addc_co_u32_e32 v87, vcc, 0, v3, vcc
	v_add_co_u32_e32 v88, vcc, s1, v2
	s_mov_b32 s1, 0xc14000
	s_nop 0
	v_addc_co_u32_e32 v89, vcc, 0, v3, vcc
	global_load_dwordx4 v[10:13], v[10:11], off sc0 nt
	s_nop 0
	global_load_dwordx4 v[18:21], v[18:19], off sc0 nt
	s_nop 0
	global_load_dwordx4 v[34:37], v[38:39], off sc0 nt
	global_load_dwordx4 v[26:29], v[40:41], off sc0 nt
	s_nop 0
	global_load_dwordx4 v[38:41], v[58:59], off sc0 nt
	global_load_dwordx4 v[50:53], v[60:61], off sc0 nt
	global_load_dwordx4 v[62:65], v[70:71], off sc0 nt
	s_nop 0
	global_load_dwordx4 v[58:61], v[72:73], off sc0 nt
	s_nop 0
	global_load_dwordx4 v[70:73], v[86:87], off sc0 nt
	global_load_dwordx4 v[82:85], v[88:89], off sc0 nt
	v_add_co_u32_e32 v86, vcc, s1, v2
	s_mov_b32 s1, 0xc16000
	s_nop 0
	v_addc_co_u32_e32 v87, vcc, 0, v3, vcc
	v_add_co_u32_e32 v88, vcc, s1, v2
	s_mov_b32 s1, 0xc18000
	s_nop 0
	v_addc_co_u32_e32 v89, vcc, 0, v3, vcc
	v_add_co_u32_e32 v98, vcc, s1, v2
	s_mov_b32 s1, 0xc1a000
	s_nop 0
	v_addc_co_u32_e32 v99, vcc, 0, v3, vcc
	v_add_co_u32_e32 v106, vcc, s1, v2
	s_mov_b32 s1, 0xc1c000
	s_nop 0
	v_addc_co_u32_e32 v107, vcc, 0, v3, vcc
	v_add_co_u32_e32 v114, vcc, s1, v2
	s_mov_b32 s1, 0xc1e000
	s_nop 0
	v_addc_co_u32_e32 v115, vcc, 0, v3, vcc
	v_add_co_u32_e32 v116, vcc, s1, v2
	global_load_dwordx4 v[90:93], v[86:87], off sc0 nt
	s_nop 0
	global_load_dwordx4 v[86:89], v[88:89], off sc0 nt
	v_addc_co_u32_e32 v117, vcc, 0, v3, vcc
	global_load_dwordx4 v[98:101], v[98:99], off sc0 nt
	s_nop 0
	global_load_dwordx4 v[106:109], v[106:107], off sc0 nt
	s_nop 0
	global_load_dwordx4 v[122:125], v[114:115], off sc0 nt
	s_nop 0
	global_load_dwordx4 v[114:117], v[116:117], off sc0 nt
	ds_read_b128 v[130:133], v154
	ds_read_b128 v[138:141], v156
	ds_read_b128 v[142:145], v158
	ds_read_b128 v[146:149], v162
	s_waitcnt lgkmcnt(3)
	global_store_dwordx4 v[150:151], v[130:133], off offset:1024 nt
	s_waitcnt lgkmcnt(2)
	global_store_dwordx4 v[152:153], v[138:141], off offset:1024 nt
	s_waitcnt lgkmcnt(1)
	global_store_dwordx4 v[160:161], v[142:145], off offset:1024 nt
	s_waitcnt lgkmcnt(0)
	global_store_dwordx4 v[164:165], v[146:149], off offset:1024 nt
	s_waitcnt vmcnt(39)
	v_mul_f32_e32 v4, 0x43800000, v6
	s_waitcnt vmcnt(38)
	v_mul_f32_e32 v6, 0x43800000, v14
	v_med3_f32 v4, v4, s0, v1
	v_med3_f32 v6, v6, s0, v1
	v_mov_b32_e32 v130, v5
	v_cvt_pk_fp8_f32 v130, v4, v6
	s_waitcnt vmcnt(37)
	v_mul_f32_e32 v14, 0x43800000, v30
	s_waitcnt vmcnt(36)
	v_mul_f32_e32 v4, 0x43800000, v22
	v_med3_f32 v6, v14, s0, v1
	v_med3_f32 v4, v4, s0, v1
	v_cvt_pk_fp8_f32 v130, v6, v4 op_sel:[0,0,1]
	s_waitcnt vmcnt(35)
	v_mul_f32_e32 v4, 0x43800000, v42
	s_waitcnt vmcnt(34)
	v_mul_f32_e32 v6, 0x43800000, v46
	v_med3_f32 v4, v4, s0, v1
	v_med3_f32 v6, v6, s0, v1
	v_mov_b32_e32 v131, v5
	v_cvt_pk_fp8_f32 v131, v4, v6
	s_waitcnt vmcnt(33)
	v_mul_f32_e32 v14, 0x43800000, v66
	s_waitcnt vmcnt(32)
	v_mul_f32_e32 v4, 0x43800000, v54
	v_med3_f32 v6, v14, s0, v1
	v_med3_f32 v4, v4, s0, v1
	v_cvt_pk_fp8_f32 v131, v6, v4 op_sel:[0,0,1]
	s_waitcnt vmcnt(31)
	v_mul_f32_e32 v4, 0x43800000, v74
	s_waitcnt vmcnt(30)
	v_mul_f32_e32 v6, 0x43800000, v78
	v_med3_f32 v4, v4, s0, v1
	v_med3_f32 v6, v6, s0, v1
	v_mov_b32_e32 v132, v5
	v_cvt_pk_fp8_f32 v132, v4, v6
	s_waitcnt vmcnt(29)
	v_mul_f32_e32 v14, 0x43800000, v102
	s_waitcnt vmcnt(28)
	v_mul_f32_e32 v4, 0x43800000, v94
	v_med3_f32 v6, v14, s0, v1
	v_med3_f32 v4, v4, s0, v1
	v_cvt_pk_fp8_f32 v132, v6, v4 op_sel:[0,0,1]
	s_waitcnt vmcnt(27)
	v_mul_f32_e32 v4, 0x43800000, v110
	s_waitcnt vmcnt(26)
	v_mul_f32_e32 v6, 0x43800000, v118
	v_med3_f32 v4, v4, s0, v1
	v_med3_f32 v6, v6, s0, v1
	v_mov_b32_e32 v133, v5
	v_cvt_pk_fp8_f32 v133, v4, v6
	s_waitcnt vmcnt(25)
	v_mul_f32_e32 v14, 0x43800000, v134
	s_waitcnt vmcnt(24)
	v_mul_f32_e32 v4, 0x43800000, v126
	v_med3_f32 v6, v14, s0, v1
	v_med3_f32 v4, v4, s0, v1
	v_cvt_pk_fp8_f32 v133, v6, v4 op_sel:[0,0,1]
	v_mul_f32_e32 v4, 0x43800000, v7
	v_mul_f32_e32 v6, 0x43800000, v15
	v_med3_f32 v4, v4, s0, v1
	v_med3_f32 v6, v6, s0, v1
	v_mov_b32_e32 v138, v5
	v_cvt_pk_fp8_f32 v138, v4, v6
	v_mul_f32_e32 v7, 0x43800000, v31
	v_mul_f32_e32 v4, 0x43800000, v23
	v_med3_f32 v6, v7, s0, v1
	v_med3_f32 v4, v4, s0, v1
	v_cvt_pk_fp8_f32 v138, v6, v4 op_sel:[0,0,1]
	v_mul_f32_e32 v4, 0x43800000, v43
	v_mul_f32_e32 v6, 0x43800000, v47
	v_med3_f32 v4, v4, s0, v1
	v_med3_f32 v6, v6, s0, v1
	v_mov_b32_e32 v139, v5
	v_cvt_pk_fp8_f32 v139, v4, v6
	v_mul_f32_e32 v7, 0x43800000, v67
	v_mul_f32_e32 v4, 0x43800000, v55
	v_med3_f32 v6, v7, s0, v1
	v_med3_f32 v4, v4, s0, v1
	v_cvt_pk_fp8_f32 v139, v6, v4 op_sel:[0,0,1]
	v_mul_f32_e32 v4, 0x43800000, v75
	v_mul_f32_e32 v6, 0x43800000, v79
	v_med3_f32 v4, v4, s0, v1
	v_med3_f32 v6, v6, s0, v1
	v_mov_b32_e32 v140, v5
	v_cvt_pk_fp8_f32 v140, v4, v6
	v_mul_f32_e32 v7, 0x43800000, v103
	v_mul_f32_e32 v4, 0x43800000, v95
	v_med3_f32 v6, v7, s0, v1
	v_med3_f32 v4, v4, s0, v1
	v_cvt_pk_fp8_f32 v140, v6, v4 op_sel:[0,0,1]
	v_mul_f32_e32 v4, 0x43800000, v111
	v_mul_f32_e32 v6, 0x43800000, v119
	v_med3_f32 v4, v4, s0, v1
	v_med3_f32 v6, v6, s0, v1
	v_mov_b32_e32 v141, v5
	v_cvt_pk_fp8_f32 v141, v4, v6
	v_mul_f32_e32 v7, 0x43800000, v135
	v_mul_f32_e32 v4, 0x43800000, v127
	v_med3_f32 v6, v7, s0, v1
	v_med3_f32 v4, v4, s0, v1
	v_cvt_pk_fp8_f32 v141, v6, v4 op_sel:[0,0,1]
	v_mul_f32_e32 v4, 0x43800000, v8
	v_mul_f32_e32 v6, 0x43800000, v16
	v_med3_f32 v4, v4, s0, v1
	v_med3_f32 v6, v6, s0, v1
	v_mov_b32_e32 v142, v5
	v_cvt_pk_fp8_f32 v142, v4, v6
	v_mul_f32_e32 v7, 0x43800000, v32
	v_mul_f32_e32 v4, 0x43800000, v24
	v_med3_f32 v6, v7, s0, v1
	v_med3_f32 v4, v4, s0, v1
	v_cvt_pk_fp8_f32 v142, v6, v4 op_sel:[0,0,1]
	v_mul_f32_e32 v4, 0x43800000, v44
	v_mul_f32_e32 v6, 0x43800000, v48
	v_med3_f32 v4, v4, s0, v1
	v_med3_f32 v6, v6, s0, v1
	v_mov_b32_e32 v143, v5
	v_cvt_pk_fp8_f32 v143, v4, v6
	v_mul_f32_e32 v7, 0x43800000, v68
	v_mul_f32_e32 v4, 0x43800000, v56
	v_med3_f32 v6, v7, s0, v1
	v_med3_f32 v4, v4, s0, v1
	v_cvt_pk_fp8_f32 v143, v6, v4 op_sel:[0,0,1]
	v_mul_f32_e32 v4, 0x43800000, v76
	v_mul_f32_e32 v6, 0x43800000, v80
	v_med3_f32 v4, v4, s0, v1
	v_med3_f32 v6, v6, s0, v1
	v_mov_b32_e32 v144, v5
	v_cvt_pk_fp8_f32 v144, v4, v6
	v_mul_f32_e32 v7, 0x43800000, v104
	v_mul_f32_e32 v4, 0x43800000, v96
	v_med3_f32 v6, v7, s0, v1
	v_med3_f32 v4, v4, s0, v1
	v_cvt_pk_fp8_f32 v144, v6, v4 op_sel:[0,0,1]
	v_mul_f32_e32 v4, 0x43800000, v112
	v_mul_f32_e32 v6, 0x43800000, v120
	v_med3_f32 v4, v4, s0, v1
	v_med3_f32 v6, v6, s0, v1
	v_mov_b32_e32 v145, v5
	v_cvt_pk_fp8_f32 v145, v4, v6
	v_mul_f32_e32 v7, 0x43800000, v136
	v_mul_f32_e32 v4, 0x43800000, v128
	v_med3_f32 v6, v7, s0, v1
	v_med3_f32 v4, v4, s0, v1
	v_cvt_pk_fp8_f32 v145, v6, v4 op_sel:[0,0,1]
	v_mul_f32_e32 v4, 0x43800000, v9
	v_mul_f32_e32 v6, 0x43800000, v17
	v_med3_f32 v4, v4, s0, v1
	v_med3_f32 v8, v6, s0, v1
	v_mov_b32_e32 v6, v5
	v_cvt_pk_fp8_f32 v6, v4, v8
	v_mul_f32_e32 v7, 0x43800000, v33
	v_mul_f32_e32 v4, 0x43800000, v25
	v_med3_f32 v7, v7, s0, v1
	v_med3_f32 v4, v4, s0, v1
	v_cvt_pk_fp8_f32 v6, v7, v4 op_sel:[0,0,1]
	v_mul_f32_e32 v4, 0x43800000, v45
	v_mul_f32_e32 v7, 0x43800000, v49
	v_med3_f32 v4, v4, s0, v1
	v_med3_f32 v9, v7, s0, v1
	v_mov_b32_e32 v7, v5
	v_cvt_pk_fp8_f32 v7, v4, v9
	v_mul_f32_e32 v8, 0x43800000, v69
	v_mul_f32_e32 v4, 0x43800000, v57
	v_med3_f32 v8, v8, s0, v1
	v_med3_f32 v4, v4, s0, v1
	v_cvt_pk_fp8_f32 v7, v8, v4 op_sel:[0,0,1]
	v_mul_f32_e32 v4, 0x43800000, v77
	v_mul_f32_e32 v8, 0x43800000, v81
	v_med3_f32 v4, v4, s0, v1
	v_med3_f32 v14, v8, s0, v1
	v_mov_b32_e32 v8, v5
	v_cvt_pk_fp8_f32 v8, v4, v14
	v_mul_f32_e32 v9, 0x43800000, v105
	v_mul_f32_e32 v4, 0x43800000, v97
	v_med3_f32 v9, v9, s0, v1
	v_med3_f32 v4, v4, s0, v1
	v_cvt_pk_fp8_f32 v8, v9, v4 op_sel:[0,0,1]
	v_mul_f32_e32 v4, 0x43800000, v113
	v_mul_f32_e32 v9, 0x43800000, v121
	v_med3_f32 v4, v4, s0, v1
	v_med3_f32 v15, v9, s0, v1
	v_mov_b32_e32 v9, v5
	v_cvt_pk_fp8_f32 v9, v4, v15
	v_mul_f32_e32 v14, 0x43800000, v137
	v_mul_f32_e32 v4, 0x43800000, v129
	v_med3_f32 v14, v14, s0, v1
	v_med3_f32 v4, v4, s0, v1
	v_cvt_pk_fp8_f32 v9, v14, v4 op_sel:[0,0,1]
	ds_write_b128 v166, v[130:133] offset:34816
	ds_write_b128 v166, v[138:141] offset:35088
	ds_write_b128 v166, v[142:145] offset:35360
	ds_write_b128 v166, v[6:9] offset:35632
	s_waitcnt lgkmcnt(0)
	s_barrier
	s_mov_b32 s1, 0xe00000
	v_add_co_u32_e32 v6, vcc, s1, v2
	s_mov_b32 s1, 0xe02000
	s_nop 0
	v_addc_co_u32_e32 v7, vcc, 0, v3, vcc
	v_add_co_u32_e32 v14, vcc, s1, v2
	s_mov_b32 s1, 0xe04000
	s_nop 0
	v_addc_co_u32_e32 v15, vcc, 0, v3, vcc
	v_add_co_u32_e32 v42, vcc, s1, v2
	s_mov_b32 s1, 0xe06000
	s_nop 0
	v_addc_co_u32_e32 v43, vcc, 0, v3, vcc
	v_add_co_u32_e32 v44, vcc, s1, v2
	s_mov_b32 s1, 0xe08000
	s_nop 0
	v_addc_co_u32_e32 v45, vcc, 0, v3, vcc
	v_add_co_u32_e32 v54, vcc, s1, v2
	s_mov_b32 s1, 0xe0a000
	s_nop 0
	v_addc_co_u32_e32 v55, vcc, 0, v3, vcc
	v_add_co_u32_e32 v56, vcc, s1, v2
	s_mov_b32 s1, 0xe0c000
	s_nop 0
	v_addc_co_u32_e32 v57, vcc, 0, v3, vcc
	v_add_co_u32_e32 v74, vcc, s1, v2
	s_mov_b32 s1, 0xe0e000
	s_nop 0
	v_addc_co_u32_e32 v75, vcc, 0, v3, vcc
	v_add_co_u32_e32 v76, vcc, s1, v2
	s_mov_b32 s1, 0xe10000
	s_nop 0
	v_addc_co_u32_e32 v77, vcc, 0, v3, vcc
	v_add_co_u32_e32 v94, vcc, s1, v2
	s_mov_b32 s1, 0xe12000
	s_nop 0
	v_addc_co_u32_e32 v95, vcc, 0, v3, vcc
	v_add_co_u32_e32 v96, vcc, s1, v2
	s_mov_b32 s1, 0xe14000
	s_nop 0
	v_addc_co_u32_e32 v97, vcc, 0, v3, vcc
	global_load_dwordx4 v[6:9], v[6:7], off sc0 nt
	s_nop 0
	global_load_dwordx4 v[14:17], v[14:15], off sc0 nt
	s_nop 0
	global_load_dwordx4 v[30:33], v[42:43], off sc0 nt
	global_load_dwordx4 v[22:25], v[44:45], off sc0 nt
	s_nop 0
	global_load_dwordx4 v[42:45], v[54:55], off sc0 nt
	global_load_dwordx4 v[46:49], v[56:57], off sc0 nt
	global_load_dwordx4 v[66:69], v[74:75], off sc0 nt
	s_nop 0
	global_load_dwordx4 v[54:57], v[76:77], off sc0 nt
	s_nop 0
	global_load_dwordx4 v[74:77], v[94:95], off sc0 nt
	global_load_dwordx4 v[78:81], v[96:97], off sc0 nt
	v_add_co_u32_e32 v94, vcc, s1, v2
	s_mov_b32 s1, 0xe16000
	s_nop 0
	v_addc_co_u32_e32 v95, vcc, 0, v3, vcc
	v_add_co_u32_e32 v96, vcc, s1, v2
	s_mov_b32 s1, 0xe18000
	s_nop 0
	v_addc_co_u32_e32 v97, vcc, 0, v3, vcc
	v_add_co_u32_e32 v110, vcc, s1, v2
	s_mov_b32 s1, 0xe1a000
	s_nop 0
	v_addc_co_u32_e32 v111, vcc, 0, v3, vcc
	v_add_co_u32_e32 v118, vcc, s1, v2
	s_mov_b32 s1, 0xe1c000
	s_nop 0
	v_addc_co_u32_e32 v119, vcc, 0, v3, vcc
	v_add_co_u32_e32 v126, vcc, s1, v2
	s_mov_b32 s1, 0xe1e000
	s_nop 0
	v_addc_co_u32_e32 v127, vcc, 0, v3, vcc
	v_add_co_u32_e32 v2, vcc, s1, v2
	global_load_dwordx4 v[102:105], v[94:95], off sc0 nt
	s_nop 0
	global_load_dwordx4 v[94:97], v[96:97], off sc0 nt
	s_nop 0
	global_load_dwordx4 v[110:113], v[110:111], off sc0 nt
	s_nop 0
	global_load_dwordx4 v[118:121], v[118:119], off sc0 nt
	v_addc_co_u32_e32 v3, vcc, 0, v3, vcc
	global_load_dwordx4 v[130:133], v[126:127], off sc0 nt
	s_nop 0
	global_load_dwordx4 v[126:129], v[2:3], off sc0 nt
	ds_read_b128 v[134:137], v154 offset:34816
	ds_read_b128 v[138:141], v156 offset:34816
	ds_read_b128 v[142:145], v158 offset:34816
	ds_read_b128 v[146:149], v162 offset:34816
	s_waitcnt lgkmcnt(3)
	global_store_dwordx4 v[150:151], v[134:137], off offset:1280 nt
	s_waitcnt lgkmcnt(2)
	global_store_dwordx4 v[152:153], v[138:141], off offset:1280 nt
	s_waitcnt lgkmcnt(1)
	global_store_dwordx4 v[160:161], v[142:145], off offset:1280 nt
	s_waitcnt lgkmcnt(0)
	global_store_dwordx4 v[164:165], v[146:149], off offset:1280 nt
	s_waitcnt vmcnt(39)
	v_mul_f32_e32 v2, 0x43800000, v10
	s_waitcnt vmcnt(38)
	v_mul_f32_e32 v3, 0x43800000, v18
	v_med3_f32 v2, v2, s0, v1
	v_med3_f32 v3, v3, s0, v1
	v_mov_b32_e32 v134, v5
	v_cvt_pk_fp8_f32 v134, v2, v3
	s_waitcnt vmcnt(37)
	v_mul_f32_e32 v4, 0x43800000, v34
	s_waitcnt vmcnt(36)
	v_mul_f32_e32 v2, 0x43800000, v26
	v_med3_f32 v3, v4, s0, v1
	v_med3_f32 v2, v2, s0, v1
	v_cvt_pk_fp8_f32 v134, v3, v2 op_sel:[0,0,1]
	s_waitcnt vmcnt(35)
	v_mul_f32_e32 v2, 0x43800000, v38
	s_waitcnt vmcnt(34)
	v_mul_f32_e32 v3, 0x43800000, v50
	v_med3_f32 v2, v2, s0, v1
	v_med3_f32 v3, v3, s0, v1
	v_mov_b32_e32 v135, v5
	v_cvt_pk_fp8_f32 v135, v2, v3
	s_waitcnt vmcnt(33)
	v_mul_f32_e32 v4, 0x43800000, v62
	s_waitcnt vmcnt(32)
	v_mul_f32_e32 v2, 0x43800000, v58
	v_med3_f32 v3, v4, s0, v1
	v_med3_f32 v2, v2, s0, v1
	v_cvt_pk_fp8_f32 v135, v3, v2 op_sel:[0,0,1]
	s_waitcnt vmcnt(31)
	v_mul_f32_e32 v2, 0x43800000, v70
	s_waitcnt vmcnt(30)
	v_mul_f32_e32 v3, 0x43800000, v82
	v_med3_f32 v2, v2, s0, v1
	v_med3_f32 v3, v3, s0, v1
	v_mov_b32_e32 v136, v5
	v_cvt_pk_fp8_f32 v136, v2, v3
	s_waitcnt vmcnt(29)
	v_mul_f32_e32 v4, 0x43800000, v90
	s_waitcnt vmcnt(28)
	v_mul_f32_e32 v2, 0x43800000, v86
	v_med3_f32 v3, v4, s0, v1
	v_med3_f32 v2, v2, s0, v1
	v_cvt_pk_fp8_f32 v136, v3, v2 op_sel:[0,0,1]
	s_waitcnt vmcnt(27)
	v_mul_f32_e32 v2, 0x43800000, v98
	s_waitcnt vmcnt(26)
	v_mul_f32_e32 v3, 0x43800000, v106
	v_med3_f32 v2, v2, s0, v1
	v_med3_f32 v3, v3, s0, v1
	v_mov_b32_e32 v137, v5
	v_cvt_pk_fp8_f32 v137, v2, v3
	s_waitcnt vmcnt(25)
	v_mul_f32_e32 v4, 0x43800000, v122
	s_waitcnt vmcnt(24)
	v_mul_f32_e32 v2, 0x43800000, v114
	v_med3_f32 v3, v4, s0, v1
	v_med3_f32 v2, v2, s0, v1
	v_cvt_pk_fp8_f32 v137, v3, v2 op_sel:[0,0,1]
	v_mul_f32_e32 v2, 0x43800000, v11
	v_mul_f32_e32 v3, 0x43800000, v19
	v_med3_f32 v2, v2, s0, v1
	v_med3_f32 v3, v3, s0, v1
	v_mov_b32_e32 v138, v5
	v_cvt_pk_fp8_f32 v138, v2, v3
	v_mul_f32_e32 v4, 0x43800000, v35
	v_mul_f32_e32 v2, 0x43800000, v27
	v_med3_f32 v3, v4, s0, v1
	v_med3_f32 v2, v2, s0, v1
	v_cvt_pk_fp8_f32 v138, v3, v2 op_sel:[0,0,1]
	v_mul_f32_e32 v2, 0x43800000, v39
	v_mul_f32_e32 v3, 0x43800000, v51
	v_med3_f32 v2, v2, s0, v1
	v_med3_f32 v3, v3, s0, v1
	v_mov_b32_e32 v139, v5
	v_cvt_pk_fp8_f32 v139, v2, v3
	v_mul_f32_e32 v4, 0x43800000, v63
	v_mul_f32_e32 v2, 0x43800000, v59
	v_med3_f32 v3, v4, s0, v1
	v_med3_f32 v2, v2, s0, v1
	v_cvt_pk_fp8_f32 v139, v3, v2 op_sel:[0,0,1]
	v_mul_f32_e32 v2, 0x43800000, v71
	v_mul_f32_e32 v3, 0x43800000, v83
	v_med3_f32 v2, v2, s0, v1
	v_med3_f32 v3, v3, s0, v1
	v_mov_b32_e32 v140, v5
	v_cvt_pk_fp8_f32 v140, v2, v3
	v_mul_f32_e32 v4, 0x43800000, v91
	v_mul_f32_e32 v2, 0x43800000, v87
	v_med3_f32 v3, v4, s0, v1
	v_med3_f32 v2, v2, s0, v1
	v_cvt_pk_fp8_f32 v140, v3, v2 op_sel:[0,0,1]
	v_mul_f32_e32 v2, 0x43800000, v99
	v_mul_f32_e32 v3, 0x43800000, v107
	v_med3_f32 v2, v2, s0, v1
	v_med3_f32 v3, v3, s0, v1
	v_mov_b32_e32 v141, v5
	v_cvt_pk_fp8_f32 v141, v2, v3
	v_mul_f32_e32 v4, 0x43800000, v123
	v_mul_f32_e32 v2, 0x43800000, v115
	v_med3_f32 v3, v4, s0, v1
	v_med3_f32 v2, v2, s0, v1
	v_cvt_pk_fp8_f32 v141, v3, v2 op_sel:[0,0,1]
	v_mul_f32_e32 v2, 0x43800000, v12
	v_mul_f32_e32 v3, 0x43800000, v20
	v_med3_f32 v2, v2, s0, v1
	v_med3_f32 v3, v3, s0, v1
	v_mov_b32_e32 v142, v5
	v_cvt_pk_fp8_f32 v142, v2, v3
	v_mul_f32_e32 v4, 0x43800000, v36
	v_mul_f32_e32 v2, 0x43800000, v28
	v_med3_f32 v3, v4, s0, v1
	v_med3_f32 v2, v2, s0, v1
	v_cvt_pk_fp8_f32 v142, v3, v2 op_sel:[0,0,1]
	v_mul_f32_e32 v2, 0x43800000, v40
	v_mul_f32_e32 v3, 0x43800000, v52
	v_med3_f32 v2, v2, s0, v1
	v_med3_f32 v3, v3, s0, v1
	v_mov_b32_e32 v143, v5
	v_cvt_pk_fp8_f32 v143, v2, v3
	v_mul_f32_e32 v4, 0x43800000, v64
	v_mul_f32_e32 v2, 0x43800000, v60
	v_med3_f32 v3, v4, s0, v1
	v_med3_f32 v2, v2, s0, v1
	v_cvt_pk_fp8_f32 v143, v3, v2 op_sel:[0,0,1]
	v_mul_f32_e32 v2, 0x43800000, v72
	v_mul_f32_e32 v3, 0x43800000, v84
	v_med3_f32 v2, v2, s0, v1
	v_med3_f32 v3, v3, s0, v1
	v_mov_b32_e32 v144, v5
	v_cvt_pk_fp8_f32 v144, v2, v3
	v_mul_f32_e32 v4, 0x43800000, v92
	v_mul_f32_e32 v2, 0x43800000, v88
	v_med3_f32 v3, v4, s0, v1
	v_med3_f32 v2, v2, s0, v1
	v_cvt_pk_fp8_f32 v144, v3, v2 op_sel:[0,0,1]
	v_mul_f32_e32 v2, 0x43800000, v100
	v_mul_f32_e32 v3, 0x43800000, v108
	v_med3_f32 v2, v2, s0, v1
	v_med3_f32 v3, v3, s0, v1
	v_mov_b32_e32 v145, v5
	v_cvt_pk_fp8_f32 v145, v2, v3
	v_mul_f32_e32 v4, 0x43800000, v124
	v_mul_f32_e32 v2, 0x43800000, v116
	v_med3_f32 v3, v4, s0, v1
	v_med3_f32 v2, v2, s0, v1
	v_cvt_pk_fp8_f32 v145, v3, v2 op_sel:[0,0,1]
	v_mul_f32_e32 v2, 0x43800000, v13
	v_mul_f32_e32 v3, 0x43800000, v21
	v_med3_f32 v2, v2, s0, v1
	v_med3_f32 v3, v3, s0, v1
	v_mov_b32_e32 v10, v5
	v_cvt_pk_fp8_f32 v10, v2, v3
	v_mul_f32_e32 v4, 0x43800000, v37
	v_mul_f32_e32 v2, 0x43800000, v29
	v_med3_f32 v3, v4, s0, v1
	v_med3_f32 v2, v2, s0, v1
	v_cvt_pk_fp8_f32 v10, v3, v2 op_sel:[0,0,1]
	v_mul_f32_e32 v2, 0x43800000, v41
	v_mul_f32_e32 v3, 0x43800000, v53
	v_med3_f32 v2, v2, s0, v1
	v_med3_f32 v3, v3, s0, v1
	v_mov_b32_e32 v11, v5
	v_cvt_pk_fp8_f32 v11, v2, v3
	v_mul_f32_e32 v4, 0x43800000, v65
	v_mul_f32_e32 v2, 0x43800000, v61
	v_med3_f32 v3, v4, s0, v1
	v_med3_f32 v2, v2, s0, v1
	v_cvt_pk_fp8_f32 v11, v3, v2 op_sel:[0,0,1]
	v_mul_f32_e32 v2, 0x43800000, v73
	v_mul_f32_e32 v3, 0x43800000, v85
	v_med3_f32 v2, v2, s0, v1
	v_med3_f32 v3, v3, s0, v1
	v_mov_b32_e32 v12, v5
	v_cvt_pk_fp8_f32 v12, v2, v3
	v_mul_f32_e32 v4, 0x43800000, v93
	v_mul_f32_e32 v2, 0x43800000, v89
	v_med3_f32 v3, v4, s0, v1
	v_med3_f32 v2, v2, s0, v1
	v_cvt_pk_fp8_f32 v12, v3, v2 op_sel:[0,0,1]
	v_mul_f32_e32 v2, 0x43800000, v101
	v_mul_f32_e32 v3, 0x43800000, v109
	v_med3_f32 v2, v2, s0, v1
	v_med3_f32 v3, v3, s0, v1
	v_mov_b32_e32 v13, v5
	v_cvt_pk_fp8_f32 v13, v2, v3
	v_mul_f32_e32 v4, 0x43800000, v125
	v_mul_f32_e32 v2, 0x43800000, v117
	v_med3_f32 v3, v4, s0, v1
	v_med3_f32 v2, v2, s0, v1
	v_cvt_pk_fp8_f32 v13, v3, v2 op_sel:[0,0,1]
	ds_write_b128 v166, v[134:137]
	ds_write_b128 v166, v[138:141] offset:272
	ds_write_b128 v166, v[142:145] offset:544
	ds_write_b128 v166, v[10:13] offset:816
	s_waitcnt lgkmcnt(0)
	s_barrier
	ds_read_b128 v[10:13], v154
	ds_read_b128 v[18:21], v156
	ds_read_b128 v[26:29], v158
	ds_read_b128 v[34:37], v162
	s_waitcnt lgkmcnt(3)
	global_store_dwordx4 v[150:151], v[10:13], off offset:1536 nt
	s_waitcnt lgkmcnt(2)
	global_store_dwordx4 v[152:153], v[18:21], off offset:1536 nt
	s_waitcnt lgkmcnt(1)
	global_store_dwordx4 v[160:161], v[26:29], off offset:1536 nt
	s_waitcnt lgkmcnt(0)
	global_store_dwordx4 v[164:165], v[34:37], off offset:1536 nt
	s_waitcnt vmcnt(23)
	v_mul_f32_e32 v2, 0x43800000, v6
	s_waitcnt vmcnt(22)
	v_mul_f32_e32 v3, 0x43800000, v14
	v_med3_f32 v2, v2, s0, v1
	v_med3_f32 v3, v3, s0, v1
	v_mov_b32_e32 v10, v5
	v_cvt_pk_fp8_f32 v10, v2, v3
	s_waitcnt vmcnt(21)
	v_mul_f32_e32 v4, 0x43800000, v30
	s_waitcnt vmcnt(20)
	v_mul_f32_e32 v2, 0x43800000, v22
	v_med3_f32 v3, v4, s0, v1
	v_med3_f32 v2, v2, s0, v1
	v_cvt_pk_fp8_f32 v10, v3, v2 op_sel:[0,0,1]
	s_waitcnt vmcnt(19)
	v_mul_f32_e32 v2, 0x43800000, v42
	s_waitcnt vmcnt(18)
	v_mul_f32_e32 v3, 0x43800000, v46
	v_med3_f32 v2, v2, s0, v1
	v_med3_f32 v3, v3, s0, v1
	v_mov_b32_e32 v11, v5
	v_cvt_pk_fp8_f32 v11, v2, v3
	s_waitcnt vmcnt(17)
	v_mul_f32_e32 v4, 0x43800000, v66
	s_waitcnt vmcnt(16)
	v_mul_f32_e32 v2, 0x43800000, v54
	v_med3_f32 v3, v4, s0, v1
	v_med3_f32 v2, v2, s0, v1
	v_cvt_pk_fp8_f32 v11, v3, v2 op_sel:[0,0,1]
	s_waitcnt vmcnt(15)
	v_mul_f32_e32 v2, 0x43800000, v74
	s_waitcnt vmcnt(14)
	v_mul_f32_e32 v3, 0x43800000, v78
	v_med3_f32 v2, v2, s0, v1
	v_med3_f32 v3, v3, s0, v1
	v_mov_b32_e32 v12, v5
	v_cvt_pk_fp8_f32 v12, v2, v3
	s_waitcnt vmcnt(13)
	v_mul_f32_e32 v4, 0x43800000, v102
	s_waitcnt vmcnt(12)
	v_mul_f32_e32 v2, 0x43800000, v94
	v_med3_f32 v3, v4, s0, v1
	v_med3_f32 v2, v2, s0, v1
	v_cvt_pk_fp8_f32 v12, v3, v2 op_sel:[0,0,1]
	s_waitcnt vmcnt(11)
	v_mul_f32_e32 v2, 0x43800000, v110
	s_waitcnt vmcnt(10)
	v_mul_f32_e32 v3, 0x43800000, v118
	v_med3_f32 v2, v2, s0, v1
	v_med3_f32 v3, v3, s0, v1
	v_mov_b32_e32 v13, v5
	v_cvt_pk_fp8_f32 v13, v2, v3
	s_waitcnt vmcnt(9)
	v_mul_f32_e32 v4, 0x43800000, v130
	s_waitcnt vmcnt(8)
	v_mul_f32_e32 v2, 0x43800000, v126
	v_med3_f32 v3, v4, s0, v1
	v_med3_f32 v2, v2, s0, v1
	v_cvt_pk_fp8_f32 v13, v3, v2 op_sel:[0,0,1]
	v_mul_f32_e32 v2, 0x43800000, v7
	v_mul_f32_e32 v3, 0x43800000, v15
	v_med3_f32 v2, v2, s0, v1
	v_med3_f32 v3, v3, s0, v1
	v_mov_b32_e32 v18, v5
	v_cvt_pk_fp8_f32 v18, v2, v3
	v_mul_f32_e32 v4, 0x43800000, v31
	v_mul_f32_e32 v2, 0x43800000, v23
	v_med3_f32 v3, v4, s0, v1
	v_med3_f32 v2, v2, s0, v1
	v_cvt_pk_fp8_f32 v18, v3, v2 op_sel:[0,0,1]
	v_mul_f32_e32 v2, 0x43800000, v43
	v_mul_f32_e32 v3, 0x43800000, v47
	v_med3_f32 v2, v2, s0, v1
	v_med3_f32 v3, v3, s0, v1
	v_mov_b32_e32 v19, v5
	v_cvt_pk_fp8_f32 v19, v2, v3
	v_mul_f32_e32 v4, 0x43800000, v67
	v_mul_f32_e32 v2, 0x43800000, v55
	v_med3_f32 v3, v4, s0, v1
	v_med3_f32 v2, v2, s0, v1
	v_cvt_pk_fp8_f32 v19, v3, v2 op_sel:[0,0,1]
	v_mul_f32_e32 v2, 0x43800000, v75
	v_mul_f32_e32 v3, 0x43800000, v79
	v_med3_f32 v2, v2, s0, v1
	v_med3_f32 v3, v3, s0, v1
	v_mov_b32_e32 v20, v5
	v_cvt_pk_fp8_f32 v20, v2, v3
	v_mul_f32_e32 v4, 0x43800000, v103
	v_mul_f32_e32 v2, 0x43800000, v95
	v_med3_f32 v3, v4, s0, v1
	v_med3_f32 v2, v2, s0, v1
	v_cvt_pk_fp8_f32 v20, v3, v2 op_sel:[0,0,1]
	v_mul_f32_e32 v2, 0x43800000, v111
	v_mul_f32_e32 v3, 0x43800000, v119
	v_med3_f32 v2, v2, s0, v1
	v_med3_f32 v3, v3, s0, v1
	v_mov_b32_e32 v21, v5
	v_cvt_pk_fp8_f32 v21, v2, v3
	v_mul_f32_e32 v4, 0x43800000, v131
	v_mul_f32_e32 v2, 0x43800000, v127
	v_med3_f32 v3, v4, s0, v1
	v_med3_f32 v2, v2, s0, v1
	v_cvt_pk_fp8_f32 v21, v3, v2 op_sel:[0,0,1]
	v_mul_f32_e32 v2, 0x43800000, v8
	v_mul_f32_e32 v3, 0x43800000, v16
	v_med3_f32 v2, v2, s0, v1
	v_med3_f32 v3, v3, s0, v1
	v_mov_b32_e32 v26, v5
	v_cvt_pk_fp8_f32 v26, v2, v3
	v_mul_f32_e32 v4, 0x43800000, v32
	v_mul_f32_e32 v2, 0x43800000, v24
	v_med3_f32 v3, v4, s0, v1
	v_med3_f32 v2, v2, s0, v1
	v_cvt_pk_fp8_f32 v26, v3, v2 op_sel:[0,0,1]
	v_mul_f32_e32 v2, 0x43800000, v44
	v_mul_f32_e32 v3, 0x43800000, v48
	v_med3_f32 v2, v2, s0, v1
	v_med3_f32 v3, v3, s0, v1
	v_mov_b32_e32 v27, v5
	v_cvt_pk_fp8_f32 v27, v2, v3
	v_mul_f32_e32 v4, 0x43800000, v68
	v_mul_f32_e32 v2, 0x43800000, v56
	v_med3_f32 v3, v4, s0, v1
	v_med3_f32 v2, v2, s0, v1
	v_cvt_pk_fp8_f32 v27, v3, v2 op_sel:[0,0,1]
	v_mul_f32_e32 v2, 0x43800000, v76
	v_mul_f32_e32 v3, 0x43800000, v80
	v_med3_f32 v2, v2, s0, v1
	v_med3_f32 v3, v3, s0, v1
	v_mov_b32_e32 v28, v5
	v_cvt_pk_fp8_f32 v28, v2, v3
	v_mul_f32_e32 v4, 0x43800000, v104
	v_mul_f32_e32 v2, 0x43800000, v96
	v_med3_f32 v3, v4, s0, v1
	v_med3_f32 v2, v2, s0, v1
	v_cvt_pk_fp8_f32 v28, v3, v2 op_sel:[0,0,1]
	v_mul_f32_e32 v2, 0x43800000, v112
	v_mul_f32_e32 v3, 0x43800000, v120
	v_med3_f32 v2, v2, s0, v1
	v_med3_f32 v3, v3, s0, v1
	v_mov_b32_e32 v29, v5
	v_cvt_pk_fp8_f32 v29, v2, v3
	v_mul_f32_e32 v4, 0x43800000, v132
	v_mul_f32_e32 v2, 0x43800000, v128
	v_med3_f32 v3, v4, s0, v1
	v_med3_f32 v2, v2, s0, v1
	v_cvt_pk_fp8_f32 v29, v3, v2 op_sel:[0,0,1]
	v_mul_f32_e32 v2, 0x43800000, v9
	v_mul_f32_e32 v3, 0x43800000, v17
	v_med3_f32 v6, v2, s0, v1
	v_med3_f32 v3, v3, s0, v1
	v_mov_b32_e32 v2, v5
	v_cvt_pk_fp8_f32 v2, v6, v3
	v_mul_f32_e32 v4, 0x43800000, v33
	v_mul_f32_e32 v3, 0x43800000, v25
	v_med3_f32 v4, v4, s0, v1
	v_med3_f32 v3, v3, s0, v1
	v_cvt_pk_fp8_f32 v2, v4, v3 op_sel:[0,0,1]
	v_mul_f32_e32 v3, 0x43800000, v45
	v_mul_f32_e32 v4, 0x43800000, v49
	v_med3_f32 v7, v3, s0, v1
	v_med3_f32 v4, v4, s0, v1
	v_mov_b32_e32 v3, v5
	v_cvt_pk_fp8_f32 v3, v7, v4
	v_mul_f32_e32 v6, 0x43800000, v69
	v_mul_f32_e32 v4, 0x43800000, v57
	v_med3_f32 v6, v6, s0, v1
	v_med3_f32 v4, v4, s0, v1
	v_cvt_pk_fp8_f32 v3, v6, v4 op_sel:[0,0,1]
	v_mul_f32_e32 v4, 0x43800000, v77
	v_mul_f32_e32 v6, 0x43800000, v81
	v_med3_f32 v8, v4, s0, v1
	v_med3_f32 v6, v6, s0, v1
	v_mov_b32_e32 v4, v5
	v_cvt_pk_fp8_f32 v4, v8, v6
	v_mul_f32_e32 v7, 0x43800000, v105
	v_mul_f32_e32 v6, 0x43800000, v97
	v_med3_f32 v7, v7, s0, v1
	v_med3_f32 v6, v6, s0, v1
	v_cvt_pk_fp8_f32 v4, v7, v6 op_sel:[0,0,1]
	v_mul_f32_e32 v6, 0x43800000, v113
	v_mul_f32_e32 v7, 0x43800000, v121
	v_med3_f32 v6, v6, s0, v1
	v_med3_f32 v7, v7, s0, v1
	v_cvt_pk_fp8_f32 v5, v6, v7
	v_mul_f32_e32 v8, 0x43800000, v133
	v_mul_f32_e32 v6, 0x43800000, v129
	v_med3_f32 v7, v8, s0, v1
	v_med3_f32 v1, v6, s0, v1
	v_cvt_pk_fp8_f32 v5, v7, v1 op_sel:[0,0,1]
	ds_write_b128 v166, v[10:13] offset:34816
	ds_write_b128 v166, v[18:21] offset:35088
	ds_write_b128 v166, v[26:29] offset:35360
	ds_write_b128 v166, v[2:5] offset:35632
	s_waitcnt lgkmcnt(0)
	s_barrier
	ds_read_b128 v[2:5], v154 offset:34816
	ds_read_b128 v[6:9], v156 offset:34816
	ds_read_b128 v[10:13], v158 offset:34816
	ds_read_b128 v[14:17], v162 offset:34816
	s_waitcnt lgkmcnt(3)
	global_store_dwordx4 v[150:151], v[2:5], off offset:1792 nt
	s_waitcnt lgkmcnt(2)
	global_store_dwordx4 v[152:153], v[6:9], off offset:1792 nt
	s_waitcnt lgkmcnt(1)
	global_store_dwordx4 v[160:161], v[10:13], off offset:1792 nt
	s_waitcnt lgkmcnt(0)
	global_store_dwordx4 v[164:165], v[14:17], off offset:1792 nt
	s_barrier
	s_mov_b64 s[6:7], 0
.LBB0_1054:
	s_andn2_b64 vcc, exec, s[6:7]
	s_cbranch_vccnz .LBB0_1056
	s_add_i32 s0, s74, 0x400
	s_ashr_i32 s0, s0, 5
	s_ashr_i32 s1, s0, 31
	v_readlane_b32 s12, v254, 4
	s_and_b32 s4, s74, 23
	s_lshl_b64 s[2:3], s[0:1], 25
	v_readlane_b32 s14, v254, 6
	v_readlane_b32 s15, v254, 7
	s_add_u32 s2, s14, s2
	s_addc_u32 s3, s15, s3
	s_lshl_b32 s6, s74, 6
	s_lshl_b32 s7, s74, 11
	s_and_b32 s6, s6, 0x580
	s_and_b32 s7, s7, 0x800
	s_or_b32 s6, s6, s7
	s_lshl_b32 s6, s6, 2
	s_add_u32 s2, s2, s6
	s_addc_u32 s3, s3, 0
	s_lshl_b32 s4, s4, 18
	s_lshl_b64 s[0:1], s[0:1], 23
	s_add_u32 s0, s78, s0
	v_mov_b32_e32 v134, v0
	s_addc_u32 s1, s79, s1
	s_add_u32 s6, s0, s4
	v_readfirstlane_b32 s5, v134
	s_addc_u32 s7, s1, 0
	s_ashr_i32 s0, s5, 1
	v_lshrrev_b32_e32 v1, 1, v134
	s_andn2_b32 s0, s0, 31
	v_and_b32_e32 v135, 16, v1
	s_waitcnt lgkmcnt(0)
	v_or_b32_e32 v2, s0, v135
	v_ashrrev_i32_e32 v3, 31, v2
	v_lshlrev_b32_e32 v1, 2, v134
	v_lshlrev_b64 v[2:3], 14, v[2:3]
	v_and_b32_e32 v140, 0x7c, v1
	v_lshl_add_u64 v[2:3], s[2:3], 0, v[2:3]
	v_lshlrev_b32_e32 v4, 2, v140
	v_mov_b32_e32 v5, 0
	v_lshl_add_u64 v[2:3], v[2:3], 0, v[4:5]
	s_movk_i32 s1, 0x4000
	v_add_co_u32_e32 v6, vcc, s1, v2
	s_mov_b32 s1, 0x8000
	s_nop 0
	v_addc_co_u32_e32 v7, vcc, 0, v3, vcc
	global_load_dwordx4 v[34:37], v[2:3], off sc0 nt
	global_load_dwordx4 v[38:41], v[6:7], off sc0 nt
	v_add_co_u32_e32 v6, vcc, s1, v2
	s_mov_b32 s1, 0xc000
	s_nop 0
	v_addc_co_u32_e32 v7, vcc, 0, v3, vcc
	v_add_co_u32_e32 v8, vcc, s1, v2
	s_mov_b32 s1, 0x10000
	s_nop 0
	v_addc_co_u32_e32 v9, vcc, 0, v3, vcc
	global_load_dwordx4 v[58:61], v[6:7], off sc0 nt
	global_load_dwordx4 v[50:53], v[8:9], off sc0 nt
	v_add_co_u32_e32 v6, vcc, s1, v2
	s_mov_b32 s1, 0x14000
	s_nop 0
	v_addc_co_u32_e32 v7, vcc, 0, v3, vcc
	v_add_co_u32_e32 v8, vcc, s1, v2
	s_mov_b32 s1, 0x18000
	s_nop 0
	v_addc_co_u32_e32 v9, vcc, 0, v3, vcc
	global_load_dwordx4 v[62:65], v[6:7], off sc0 nt
	global_load_dwordx4 v[70:73], v[8:9], off sc0 nt
	v_add_co_u32_e32 v6, vcc, s1, v2
	s_mov_b32 s1, 0x1c000
	s_nop 0
	v_addc_co_u32_e32 v7, vcc, 0, v3, vcc
	v_add_co_u32_e32 v8, vcc, s1, v2
	s_mov_b32 s1, 0x20000
	s_nop 0
	v_addc_co_u32_e32 v9, vcc, 0, v3, vcc
	global_load_dwordx4 v[90:93], v[6:7], off sc0 nt
	global_load_dwordx4 v[74:77], v[8:9], off sc0 nt
	v_add_co_u32_e32 v6, vcc, s1, v2
	s_mov_b32 s1, 0x24000
	s_nop 0
	v_addc_co_u32_e32 v7, vcc, 0, v3, vcc
	v_add_co_u32_e32 v8, vcc, s1, v2
	s_mov_b32 s1, 0x28000
	s_nop 0
	v_addc_co_u32_e32 v9, vcc, 0, v3, vcc
	global_load_dwordx4 v[94:97], v[6:7], off sc0 nt
	global_load_dwordx4 v[98:101], v[8:9], off sc0 nt
	v_add_co_u32_e32 v6, vcc, s1, v2
	s_mov_b32 s1, 0x2c000
	s_nop 0
	v_addc_co_u32_e32 v7, vcc, 0, v3, vcc
	v_add_co_u32_e32 v8, vcc, s1, v2
	s_mov_b32 s1, 0x30000
	s_nop 0
	v_addc_co_u32_e32 v9, vcc, 0, v3, vcc
	global_load_dwordx4 v[114:117], v[6:7], off sc0 nt
	global_load_dwordx4 v[106:109], v[8:9], off sc0 nt
	v_add_co_u32_e32 v6, vcc, s1, v2
	s_mov_b32 s1, 0x34000
	s_nop 0
	v_addc_co_u32_e32 v7, vcc, 0, v3, vcc
	v_add_co_u32_e32 v8, vcc, s1, v2
	s_mov_b32 s1, 0x38000
	s_nop 0
	v_addc_co_u32_e32 v9, vcc, 0, v3, vcc
	global_load_dwordx4 v[118:121], v[6:7], off sc0 nt
	global_load_dwordx4 v[122:125], v[8:9], off sc0 nt
	v_add_co_u32_e32 v6, vcc, s1, v2
	s_mov_b32 s1, 0x3c000
	s_nop 0
	v_addc_co_u32_e32 v7, vcc, 0, v3, vcc
	v_add_co_u32_e32 v8, vcc, s1, v2
	s_mov_b32 s1, 0x400000
	s_nop 0
	v_addc_co_u32_e32 v9, vcc, 0, v3, vcc
	v_add_co_u32_e32 v14, vcc, s1, v2
	s_mov_b32 s1, 0x404000
	s_nop 0
	v_addc_co_u32_e32 v15, vcc, 0, v3, vcc
	v_add_co_u32_e32 v16, vcc, s1, v2
	s_mov_b32 s1, 0x408000
	s_nop 0
	v_addc_co_u32_e32 v17, vcc, 0, v3, vcc
	v_add_co_u32_e32 v22, vcc, s1, v2
	s_mov_b32 s1, 0x40c000
	s_nop 0
	v_addc_co_u32_e32 v23, vcc, 0, v3, vcc
	v_add_co_u32_e32 v24, vcc, s1, v2
	s_mov_b32 s1, 0x410000
	s_nop 0
	v_addc_co_u32_e32 v25, vcc, 0, v3, vcc
	v_add_co_u32_e32 v30, vcc, s1, v2
	s_mov_b32 s1, 0x414000
	s_nop 0
	v_addc_co_u32_e32 v31, vcc, 0, v3, vcc
	v_add_co_u32_e32 v32, vcc, s1, v2
	s_mov_b32 s1, 0x418000
	s_nop 0
	v_addc_co_u32_e32 v33, vcc, 0, v3, vcc
	s_waitcnt vmcnt(0)
	v_add_co_u32_e32 v46, vcc, s1, v2
	s_mov_b32 s1, 0x41c000
	s_nop 0
	v_addc_co_u32_e32 v47, vcc, 0, v3, vcc
	v_add_co_u32_e32 v48, vcc, s1, v2
	s_mov_b32 s1, 0x420000
	s_nop 0
	v_addc_co_u32_e32 v49, vcc, 0, v3, vcc
	v_add_co_u32_e32 v66, vcc, s1, v2
	s_mov_b32 s1, 0x424000
	s_nop 0
	v_addc_co_u32_e32 v67, vcc, 0, v3, vcc
	v_add_co_u32_e32 v68, vcc, s1, v2
	s_mov_b32 s1, 0x428000
	s_nop 0
	v_addc_co_u32_e32 v69, vcc, 0, v3, vcc
	v_add_co_u32_e32 v82, vcc, s1, v2
	s_mov_b32 s1, 0x42c000
	s_nop 0
	v_addc_co_u32_e32 v83, vcc, 0, v3, vcc
	v_add_co_u32_e32 v84, vcc, s1, v2
	s_mov_b32 s1, 0x430000
	s_nop 0
	v_addc_co_u32_e32 v85, vcc, 0, v3, vcc
	global_load_dwordx4 v[130:133], v[6:7], off sc0 nt
	global_load_dwordx4 v[126:129], v[8:9], off sc0 nt
	s_nop 0
	global_load_dwordx4 v[6:9], v[14:15], off sc0 nt
	global_load_dwordx4 v[10:13], v[16:17], off sc0 nt
	global_load_dwordx4 v[18:21], v[22:23], off sc0 nt
	s_nop 0
	global_load_dwordx4 v[14:17], v[24:25], off sc0 nt
	s_nop 0
	global_load_dwordx4 v[22:25], v[30:31], off sc0 nt
	global_load_dwordx4 v[26:29], v[32:33], off sc0 nt
	global_load_dwordx4 v[42:45], v[46:47], off sc0 nt
	s_nop 0
	global_load_dwordx4 v[30:33], v[48:49], off sc0 nt
	s_nop 0
	global_load_dwordx4 v[46:49], v[66:67], off sc0 nt
	global_load_dwordx4 v[54:57], v[68:69], off sc0 nt
	global_load_dwordx4 v[78:81], v[82:83], off sc0 nt
	s_nop 0
	global_load_dwordx4 v[66:69], v[84:85], off sc0 nt
	v_add_co_u32_e32 v82, vcc, s1, v2
	s_mov_b32 s1, 0x434000
	s_nop 0
	v_addc_co_u32_e32 v83, vcc, 0, v3, vcc
	v_add_co_u32_e32 v86, vcc, s1, v2
	s_mov_b32 s1, 0x438000
	s_nop 0
	v_addc_co_u32_e32 v87, vcc, 0, v3, vcc
	v_add_co_u32_e32 v102, vcc, s1, v2
	s_mov_b32 s1, 0x43c000
	s_nop 0
	v_addc_co_u32_e32 v103, vcc, 0, v3, vcc
	v_add_co_u32_e32 v104, vcc, s1, v2
	global_load_dwordx4 v[82:85], v[82:83], off sc0 nt
	s_nop 0
	global_load_dwordx4 v[86:89], v[86:87], off sc0 nt
	v_addc_co_u32_e32 v105, vcc, 0, v3, vcc
	global_load_dwordx4 v[110:113], v[102:103], off sc0 nt
	s_nop 0
	global_load_dwordx4 v[102:105], v[104:105], off sc0 nt
	v_readlane_b32 s13, v254, 5
	v_readlane_b32 s16, v254, 8
	v_readlane_b32 s17, v254, 9
	v_readlane_b32 s18, v254, 10
	v_readlane_b32 s19, v254, 11
	s_add_i32 s2, s0, 0
	v_mul_f32_e32 v4, 0x43800000, v34
	v_mul_f32_e32 v34, 0x43800000, v38
	s_mov_b32 s0, 0xc3e00000
	v_mov_b32_e32 v1, 0x43e00000
	v_med3_f32 v4, v4, s0, v1
	v_med3_f32 v34, v34, s0, v1
	v_mov_b32_e32 v136, v5
	v_cvt_pk_fp8_f32 v136, v4, v34
	v_mul_f32_e32 v38, 0x43800000, v58
	v_mul_f32_e32 v4, 0x43800000, v50
	v_med3_f32 v34, v38, s0, v1
	v_med3_f32 v4, v4, s0, v1
	v_cvt_pk_fp8_f32 v136, v34, v4 op_sel:[0,0,1]
	v_mul_f32_e32 v4, 0x43800000, v62
	v_mul_f32_e32 v34, 0x43800000, v70
	v_med3_f32 v4, v4, s0, v1
	v_med3_f32 v34, v34, s0, v1
	v_mov_b32_e32 v137, v5
	v_cvt_pk_fp8_f32 v137, v4, v34
	v_mul_f32_e32 v38, 0x43800000, v90
	v_mul_f32_e32 v4, 0x43800000, v74
	v_med3_f32 v34, v38, s0, v1
	v_med3_f32 v4, v4, s0, v1
	v_cvt_pk_fp8_f32 v137, v34, v4 op_sel:[0,0,1]
	v_mul_f32_e32 v4, 0x43800000, v94
	v_mul_f32_e32 v34, 0x43800000, v98
	v_med3_f32 v4, v4, s0, v1
	v_med3_f32 v34, v34, s0, v1
	v_mov_b32_e32 v138, v5
	v_cvt_pk_fp8_f32 v138, v4, v34
	v_mul_f32_e32 v38, 0x43800000, v114
	v_mul_f32_e32 v4, 0x43800000, v106
	v_med3_f32 v34, v38, s0, v1
	v_med3_f32 v4, v4, s0, v1
	v_cvt_pk_fp8_f32 v138, v34, v4 op_sel:[0,0,1]
	v_mul_f32_e32 v4, 0x43800000, v118
	v_mul_f32_e32 v34, 0x43800000, v122
	v_med3_f32 v4, v4, s0, v1
	v_med3_f32 v34, v34, s0, v1
	v_mov_b32_e32 v139, v5
	v_cvt_pk_fp8_f32 v139, v4, v34
	s_waitcnt vmcnt(17)
	v_mul_f32_e32 v38, 0x43800000, v130
	s_waitcnt vmcnt(16)
	v_mul_f32_e32 v4, 0x43800000, v126
	v_med3_f32 v34, v38, s0, v1
	v_med3_f32 v4, v4, s0, v1
	v_cvt_pk_fp8_f32 v139, v34, v4 op_sel:[0,0,1]
	v_mul_u32_u24_e32 v4, 0x110, v140
	v_add3_u32 v166, s2, v135, v4
	v_mul_f32_e32 v4, 0x43800000, v35
	v_mul_f32_e32 v34, 0x43800000, v39
	v_med3_f32 v4, v4, s0, v1
	v_med3_f32 v34, v34, s0, v1
	v_mov_b32_e32 v140, v5
	v_cvt_pk_fp8_f32 v140, v4, v34
	v_mul_f32_e32 v35, 0x43800000, v59
	v_mul_f32_e32 v4, 0x43800000, v51
	v_med3_f32 v34, v35, s0, v1
	v_med3_f32 v4, v4, s0, v1
	v_cvt_pk_fp8_f32 v140, v34, v4 op_sel:[0,0,1]
	v_mul_f32_e32 v4, 0x43800000, v63
	v_mul_f32_e32 v34, 0x43800000, v71
	v_med3_f32 v4, v4, s0, v1
	v_med3_f32 v34, v34, s0, v1
	v_mov_b32_e32 v141, v5
	v_cvt_pk_fp8_f32 v141, v4, v34
	v_mul_f32_e32 v35, 0x43800000, v91
	v_mul_f32_e32 v4, 0x43800000, v75
	v_med3_f32 v34, v35, s0, v1
	v_med3_f32 v4, v4, s0, v1
	v_cvt_pk_fp8_f32 v141, v34, v4 op_sel:[0,0,1]
	v_mul_f32_e32 v4, 0x43800000, v95
	v_mul_f32_e32 v34, 0x43800000, v99
	v_med3_f32 v4, v4, s0, v1
	v_med3_f32 v34, v34, s0, v1
	v_mov_b32_e32 v142, v5
	v_cvt_pk_fp8_f32 v142, v4, v34
	v_mul_f32_e32 v35, 0x43800000, v115
	v_mul_f32_e32 v4, 0x43800000, v107
	v_med3_f32 v34, v35, s0, v1
	v_med3_f32 v4, v4, s0, v1
	v_cvt_pk_fp8_f32 v142, v34, v4 op_sel:[0,0,1]
	v_mul_f32_e32 v4, 0x43800000, v119
	v_mul_f32_e32 v34, 0x43800000, v123
	v_med3_f32 v4, v4, s0, v1
	v_med3_f32 v34, v34, s0, v1
	v_mov_b32_e32 v143, v5
	v_cvt_pk_fp8_f32 v143, v4, v34
	v_mul_f32_e32 v35, 0x43800000, v131
	v_mul_f32_e32 v4, 0x43800000, v127
	v_med3_f32 v34, v35, s0, v1
	v_med3_f32 v4, v4, s0, v1
	v_cvt_pk_fp8_f32 v143, v34, v4 op_sel:[0,0,1]
	v_mul_f32_e32 v4, 0x43800000, v36
	v_mul_f32_e32 v34, 0x43800000, v40
	v_med3_f32 v4, v4, s0, v1
	v_med3_f32 v34, v34, s0, v1
	v_mov_b32_e32 v144, v5
	v_cvt_pk_fp8_f32 v144, v4, v34
	v_mul_f32_e32 v35, 0x43800000, v60
	v_mul_f32_e32 v4, 0x43800000, v52
	v_med3_f32 v34, v35, s0, v1
	v_med3_f32 v4, v4, s0, v1
	v_cvt_pk_fp8_f32 v144, v34, v4 op_sel:[0,0,1]
	v_mul_f32_e32 v4, 0x43800000, v64
	v_mul_f32_e32 v34, 0x43800000, v72
	v_med3_f32 v4, v4, s0, v1
	v_med3_f32 v34, v34, s0, v1
	v_mov_b32_e32 v145, v5
	v_cvt_pk_fp8_f32 v145, v4, v34
	v_mul_f32_e32 v35, 0x43800000, v92
	v_mul_f32_e32 v4, 0x43800000, v76
	v_med3_f32 v34, v35, s0, v1
	v_med3_f32 v4, v4, s0, v1
	v_cvt_pk_fp8_f32 v145, v34, v4 op_sel:[0,0,1]
	v_mul_f32_e32 v4, 0x43800000, v96
	v_mul_f32_e32 v34, 0x43800000, v100
	v_med3_f32 v4, v4, s0, v1
	v_med3_f32 v34, v34, s0, v1
	v_mov_b32_e32 v146, v5
	v_cvt_pk_fp8_f32 v146, v4, v34
	v_mul_f32_e32 v35, 0x43800000, v116
	v_mul_f32_e32 v4, 0x43800000, v108
	v_med3_f32 v34, v35, s0, v1
	v_med3_f32 v4, v4, s0, v1
	v_cvt_pk_fp8_f32 v146, v34, v4 op_sel:[0,0,1]
	v_mul_f32_e32 v4, 0x43800000, v120
	v_mul_f32_e32 v34, 0x43800000, v124
	v_med3_f32 v4, v4, s0, v1
	v_med3_f32 v34, v34, s0, v1
	v_mov_b32_e32 v147, v5
	v_cvt_pk_fp8_f32 v147, v4, v34
	v_mul_f32_e32 v35, 0x43800000, v132
	v_mul_f32_e32 v4, 0x43800000, v128
	v_med3_f32 v34, v35, s0, v1
	v_med3_f32 v4, v4, s0, v1
	v_cvt_pk_fp8_f32 v147, v34, v4 op_sel:[0,0,1]
	v_mul_f32_e32 v4, 0x43800000, v37
	v_mul_f32_e32 v34, 0x43800000, v41
	v_med3_f32 v4, v4, s0, v1
	v_med3_f32 v36, v34, s0, v1
	v_mov_b32_e32 v34, v5
	v_cvt_pk_fp8_f32 v34, v4, v36
	v_mul_f32_e32 v35, 0x43800000, v61
	v_mul_f32_e32 v4, 0x43800000, v53
	v_med3_f32 v35, v35, s0, v1
	v_med3_f32 v4, v4, s0, v1
	v_cvt_pk_fp8_f32 v34, v35, v4 op_sel:[0,0,1]
	v_mul_f32_e32 v4, 0x43800000, v65
	v_mul_f32_e32 v35, 0x43800000, v73
	v_med3_f32 v4, v4, s0, v1
	v_med3_f32 v37, v35, s0, v1
	v_mov_b32_e32 v35, v5
	v_cvt_pk_fp8_f32 v35, v4, v37
	v_mul_f32_e32 v36, 0x43800000, v93
	v_mul_f32_e32 v4, 0x43800000, v77
	v_med3_f32 v36, v36, s0, v1
	v_med3_f32 v4, v4, s0, v1
	v_cvt_pk_fp8_f32 v35, v36, v4 op_sel:[0,0,1]
	v_mul_f32_e32 v4, 0x43800000, v97
	v_mul_f32_e32 v36, 0x43800000, v101
	v_med3_f32 v4, v4, s0, v1
	v_med3_f32 v38, v36, s0, v1
	v_mov_b32_e32 v36, v5
	v_cvt_pk_fp8_f32 v36, v4, v38
	v_mul_f32_e32 v37, 0x43800000, v117
	v_mul_f32_e32 v4, 0x43800000, v109
	v_med3_f32 v37, v37, s0, v1
	v_med3_f32 v4, v4, s0, v1
	v_cvt_pk_fp8_f32 v36, v37, v4 op_sel:[0,0,1]
	v_mul_f32_e32 v4, 0x43800000, v121
	v_mul_f32_e32 v37, 0x43800000, v125
	v_med3_f32 v4, v4, s0, v1
	v_med3_f32 v39, v37, s0, v1
	v_mov_b32_e32 v37, v5
	v_cvt_pk_fp8_f32 v37, v4, v39
	v_mul_f32_e32 v38, 0x43800000, v133
	v_mul_f32_e32 v4, 0x43800000, v129
	v_med3_f32 v38, v38, s0, v1
	v_med3_f32 v4, v4, s0, v1
	v_cvt_pk_fp8_f32 v37, v38, v4 op_sel:[0,0,1]
	ds_write_b128 v166, v[136:139]
	ds_write_b128 v166, v[140:143] offset:272
	ds_write_b128 v166, v[144:147] offset:544
	ds_write_b128 v166, v[34:37] offset:816
	v_add_u32_e32 v34, 0x200, v134
	v_ashrrev_i32_e32 v140, 4, v34
	v_add_u32_e32 v34, 0x400, v134
	v_ashrrev_i32_e32 v144, 4, v34
	v_add_u32_e32 v34, 0x600, v134
	v_ashrrev_i32_e32 v136, 4, v134
	v_ashrrev_i32_e32 v148, 4, v34
	v_lshlrev_b32_e32 v4, 4, v134
	v_ashrrev_i32_e32 v137, 31, v136
	v_ashrrev_i32_e32 v141, 31, v140
	v_ashrrev_i32_e32 v145, 31, v144
	v_ashrrev_i32_e32 v149, 31, v148
	s_movk_i32 s1, 0x110
	s_waitcnt lgkmcnt(0)
	s_barrier
	v_and_b32_e32 v4, 0xf0, v4
	v_lshlrev_b64 v[138:139], 11, v[136:137]
	v_lshlrev_b64 v[142:143], 11, v[140:141]
	v_lshlrev_b64 v[146:147], 11, v[144:145]
	v_lshlrev_b64 v[164:165], 11, v[148:149]
	s_mov_b32 s2, 0x800000
	v_add_co_u32_e32 v34, vcc, s2, v2
	s_mov_b32 s2, 0x804000
	s_nop 0
	v_addc_co_u32_e32 v35, vcc, 0, v3, vcc
	v_add_co_u32_e32 v38, vcc, s2, v2
	s_mov_b32 s2, 0x808000
	s_nop 0
	v_addc_co_u32_e32 v39, vcc, 0, v3, vcc
	v_add_co_u32_e32 v50, vcc, s2, v2
	s_mov_b32 s2, 0x80c000
	s_nop 0
	v_addc_co_u32_e32 v51, vcc, 0, v3, vcc
	v_add_co_u32_e32 v52, vcc, s2, v2
	s_mov_b32 s2, 0x810000
	s_nop 0
	v_addc_co_u32_e32 v53, vcc, 0, v3, vcc
	v_add_co_u32_e32 v62, vcc, s2, v2
	s_mov_b32 s2, 0x814000
	s_nop 0
	v_addc_co_u32_e32 v63, vcc, 0, v3, vcc
	v_add_co_u32_e32 v70, vcc, s2, v2
	s_mov_b32 s2, 0x818000
	s_nop 0
	v_addc_co_u32_e32 v71, vcc, 0, v3, vcc
	v_add_co_u32_e32 v74, vcc, s2, v2
	s_mov_b32 s2, 0x81c000
	s_nop 0
	v_addc_co_u32_e32 v75, vcc, 0, v3, vcc
	v_add_co_u32_e32 v76, vcc, s2, v2
	s_mov_b32 s2, 0x820000
	s_nop 0
	v_addc_co_u32_e32 v77, vcc, 0, v3, vcc
	v_add_co_u32_e32 v94, vcc, s2, v2
	s_mov_b32 s2, 0x824000
	s_nop 0
	v_addc_co_u32_e32 v95, vcc, 0, v3, vcc
	v_add_co_u32_e32 v98, vcc, s2, v2
	s_mov_b32 s2, 0x828000
	s_nop 0
	v_addc_co_u32_e32 v99, vcc, 0, v3, vcc
	v_add_co_u32_e32 v106, vcc, s2, v2
	s_mov_b32 s2, 0x82c000
	s_nop 0
	v_addc_co_u32_e32 v107, vcc, 0, v3, vcc
	v_add_co_u32_e32 v108, vcc, s2, v2
	s_mov_b32 s2, 0x830000
	s_nop 0
	v_addc_co_u32_e32 v109, vcc, 0, v3, vcc
	v_add_co_u32_e32 v118, vcc, s2, v2
	s_mov_b32 s2, 0x834000
	s_nop 0
	v_addc_co_u32_e32 v119, vcc, 0, v3, vcc
	v_add_co_u32_e32 v122, vcc, s2, v2
	s_mov_b32 s2, 0x838000
	s_nop 0
	v_addc_co_u32_e32 v123, vcc, 0, v3, vcc
	v_add_co_u32_e32 v126, vcc, s2, v2
	s_mov_b32 s2, 0x83c000
	s_nop 0
	v_addc_co_u32_e32 v127, vcc, 0, v3, vcc
	v_add_co_u32_e32 v128, vcc, s2, v2
	global_load_dwordx4 v[34:37], v[34:35], off sc0 nt
	s_nop 0
	global_load_dwordx4 v[38:41], v[38:39], off sc0 nt
	v_addc_co_u32_e32 v129, vcc, 0, v3, vcc
	global_load_dwordx4 v[58:61], v[50:51], off sc0 nt
	s_nop 0
	global_load_dwordx4 v[50:53], v[52:53], off sc0 nt
	s_nop 0
	global_load_dwordx4 v[62:65], v[62:63], off sc0 nt
	s_nop 0
	global_load_dwordx4 v[70:73], v[70:71], off sc0 nt
	s_nop 0
	global_load_dwordx4 v[90:93], v[74:75], off sc0 nt
	s_nop 0
	global_load_dwordx4 v[74:77], v[76:77], off sc0 nt
	s_nop 0
	global_load_dwordx4 v[94:97], v[94:95], off sc0 nt
	s_nop 0
	global_load_dwordx4 v[98:101], v[98:99], off sc0 nt
	s_nop 0
	global_load_dwordx4 v[114:117], v[106:107], off sc0 nt
	s_nop 0
	global_load_dwordx4 v[106:109], v[108:109], off sc0 nt
	s_nop 0
	global_load_dwordx4 v[118:121], v[118:119], off sc0 nt
	s_nop 0
	global_load_dwordx4 v[122:125], v[122:123], off sc0 nt
	s_nop 0
	global_load_dwordx4 v[130:133], v[126:127], off sc0 nt
	s_nop 0
	global_load_dwordx4 v[126:129], v[128:129], off sc0 nt
	v_add_u32_e32 v160, 0, v4
	v_lshl_add_u64 v[134:135], s[6:7], 0, v[4:5]
	s_mov_b64 s[2:3], 0x40000000
	v_lshl_add_u64 v[168:169], v[134:135], 0, s[2:3]
	v_mad_u64_u32 v[154:155], s[2:3], v136, s1, v[160:161]
	ds_read_b128 v[134:137], v154
	v_lshl_add_u64 v[150:151], v[168:169], 0, v[138:139]
	v_mad_u64_u32 v[156:157], s[2:3], v140, s1, v[160:161]
	v_mad_u64_u32 v[158:159], s[2:3], v144, s1, v[160:161]
	v_mad_u64_u32 v[162:163], s[2:3], v148, s1, v[160:161]
	ds_read_b128 v[138:141], v156
	s_waitcnt lgkmcnt(1)
	global_store_dwordx4 v[150:151], v[134:137], off nt
	v_lshl_add_u64 v[152:153], v[168:169], 0, v[142:143]
	ds_read_b128 v[134:137], v158
	ds_read_b128 v[142:145], v162
	v_lshl_add_u64 v[160:161], v[168:169], 0, v[146:147]
	v_lshl_add_u64 v[164:165], v[168:169], 0, v[164:165]
	s_waitcnt lgkmcnt(2)
	global_store_dwordx4 v[152:153], v[138:141], off nt
	s_waitcnt lgkmcnt(1)
	global_store_dwordx4 v[160:161], v[134:137], off nt
	s_waitcnt lgkmcnt(0)
	global_store_dwordx4 v[164:165], v[142:145], off nt
	s_waitcnt vmcnt(35)
	v_mul_f32_e32 v4, 0x43800000, v6
	s_waitcnt vmcnt(34)
	v_mul_f32_e32 v6, 0x43800000, v10
	v_med3_f32 v4, v4, s0, v1
	v_med3_f32 v6, v6, s0, v1
	v_mov_b32_e32 v134, v5
	v_cvt_pk_fp8_f32 v134, v4, v6
	s_waitcnt vmcnt(33)
	v_mul_f32_e32 v10, 0x43800000, v18
	s_waitcnt vmcnt(32)
	v_mul_f32_e32 v4, 0x43800000, v14
	v_med3_f32 v6, v10, s0, v1
	v_med3_f32 v4, v4, s0, v1
	v_cvt_pk_fp8_f32 v134, v6, v4 op_sel:[0,0,1]
	s_waitcnt vmcnt(31)
	v_mul_f32_e32 v4, 0x43800000, v22
	s_waitcnt vmcnt(30)
	v_mul_f32_e32 v6, 0x43800000, v26
	v_med3_f32 v4, v4, s0, v1
	v_med3_f32 v6, v6, s0, v1
	v_mov_b32_e32 v135, v5
	v_cvt_pk_fp8_f32 v135, v4, v6
	s_waitcnt vmcnt(29)
	v_mul_f32_e32 v10, 0x43800000, v42
	s_waitcnt vmcnt(28)
	v_mul_f32_e32 v4, 0x43800000, v30
	v_med3_f32 v6, v10, s0, v1
	v_med3_f32 v4, v4, s0, v1
	v_cvt_pk_fp8_f32 v135, v6, v4 op_sel:[0,0,1]
	s_waitcnt vmcnt(27)
	v_mul_f32_e32 v4, 0x43800000, v46
	s_waitcnt vmcnt(26)
	v_mul_f32_e32 v6, 0x43800000, v54
	v_med3_f32 v4, v4, s0, v1
	v_med3_f32 v6, v6, s0, v1
	v_mov_b32_e32 v136, v5
	v_cvt_pk_fp8_f32 v136, v4, v6
	s_waitcnt vmcnt(25)
	v_mul_f32_e32 v10, 0x43800000, v78
	s_waitcnt vmcnt(24)
	v_mul_f32_e32 v4, 0x43800000, v66
	v_med3_f32 v6, v10, s0, v1
	v_med3_f32 v4, v4, s0, v1
	v_cvt_pk_fp8_f32 v136, v6, v4 op_sel:[0,0,1]
	s_waitcnt vmcnt(23)
	v_mul_f32_e32 v4, 0x43800000, v82
	s_waitcnt vmcnt(22)
	v_mul_f32_e32 v6, 0x43800000, v86
	v_med3_f32 v4, v4, s0, v1
	v_med3_f32 v6, v6, s0, v1
	v_mov_b32_e32 v137, v5
	v_cvt_pk_fp8_f32 v137, v4, v6
	s_waitcnt vmcnt(21)
	v_mul_f32_e32 v10, 0x43800000, v110
	s_waitcnt vmcnt(20)
	v_mul_f32_e32 v4, 0x43800000, v102
	v_med3_f32 v6, v10, s0, v1
	v_med3_f32 v4, v4, s0, v1
	v_cvt_pk_fp8_f32 v137, v6, v4 op_sel:[0,0,1]
	v_mul_f32_e32 v4, 0x43800000, v7
	v_mul_f32_e32 v6, 0x43800000, v11
	v_med3_f32 v4, v4, s0, v1
	v_med3_f32 v6, v6, s0, v1
	v_mov_b32_e32 v138, v5
	v_cvt_pk_fp8_f32 v138, v4, v6
	v_mul_f32_e32 v7, 0x43800000, v19
	v_mul_f32_e32 v4, 0x43800000, v15
	v_med3_f32 v6, v7, s0, v1
	v_med3_f32 v4, v4, s0, v1
	v_cvt_pk_fp8_f32 v138, v6, v4 op_sel:[0,0,1]
	v_mul_f32_e32 v4, 0x43800000, v23
	v_mul_f32_e32 v6, 0x43800000, v27
	v_med3_f32 v4, v4, s0, v1
	v_med3_f32 v6, v6, s0, v1
	v_mov_b32_e32 v139, v5
	v_cvt_pk_fp8_f32 v139, v4, v6
	v_mul_f32_e32 v7, 0x43800000, v43
	v_mul_f32_e32 v4, 0x43800000, v31
	v_med3_f32 v6, v7, s0, v1
	v_med3_f32 v4, v4, s0, v1
	v_cvt_pk_fp8_f32 v139, v6, v4 op_sel:[0,0,1]
	v_mul_f32_e32 v4, 0x43800000, v47
	v_mul_f32_e32 v6, 0x43800000, v55
	v_med3_f32 v4, v4, s0, v1
	v_med3_f32 v6, v6, s0, v1
	v_mov_b32_e32 v140, v5
	v_cvt_pk_fp8_f32 v140, v4, v6
	v_mul_f32_e32 v7, 0x43800000, v79
	v_mul_f32_e32 v4, 0x43800000, v67
	v_med3_f32 v6, v7, s0, v1
	v_med3_f32 v4, v4, s0, v1
	v_cvt_pk_fp8_f32 v140, v6, v4 op_sel:[0,0,1]
	v_mul_f32_e32 v4, 0x43800000, v83
	v_mul_f32_e32 v6, 0x43800000, v87
	v_med3_f32 v4, v4, s0, v1
	v_med3_f32 v6, v6, s0, v1
	v_mov_b32_e32 v141, v5
	v_cvt_pk_fp8_f32 v141, v4, v6
	v_mul_f32_e32 v7, 0x43800000, v111
	v_mul_f32_e32 v4, 0x43800000, v103
	v_med3_f32 v6, v7, s0, v1
	v_med3_f32 v4, v4, s0, v1
	v_cvt_pk_fp8_f32 v141, v6, v4 op_sel:[0,0,1]
	v_mul_f32_e32 v4, 0x43800000, v8
	v_mul_f32_e32 v6, 0x43800000, v12
	v_med3_f32 v4, v4, s0, v1
	v_med3_f32 v6, v6, s0, v1
	v_mov_b32_e32 v142, v5
	v_cvt_pk_fp8_f32 v142, v4, v6
	v_mul_f32_e32 v7, 0x43800000, v20
	v_mul_f32_e32 v4, 0x43800000, v16
	v_med3_f32 v6, v7, s0, v1
	v_med3_f32 v4, v4, s0, v1
	v_cvt_pk_fp8_f32 v142, v6, v4 op_sel:[0,0,1]
	v_mul_f32_e32 v4, 0x43800000, v24
	v_mul_f32_e32 v6, 0x43800000, v28
	v_med3_f32 v4, v4, s0, v1
	v_med3_f32 v6, v6, s0, v1
	v_mov_b32_e32 v143, v5
	v_cvt_pk_fp8_f32 v143, v4, v6
	v_mul_f32_e32 v7, 0x43800000, v44
	v_mul_f32_e32 v4, 0x43800000, v32
	v_med3_f32 v6, v7, s0, v1
	v_med3_f32 v4, v4, s0, v1
	v_cvt_pk_fp8_f32 v143, v6, v4 op_sel:[0,0,1]
	v_mul_f32_e32 v4, 0x43800000, v48
	v_mul_f32_e32 v6, 0x43800000, v56
	v_med3_f32 v4, v4, s0, v1
	v_med3_f32 v6, v6, s0, v1
	v_mov_b32_e32 v144, v5
	v_cvt_pk_fp8_f32 v144, v4, v6
	v_mul_f32_e32 v7, 0x43800000, v80
	v_mul_f32_e32 v4, 0x43800000, v68
	v_med3_f32 v6, v7, s0, v1
	v_med3_f32 v4, v4, s0, v1
	v_cvt_pk_fp8_f32 v144, v6, v4 op_sel:[0,0,1]
	v_mul_f32_e32 v4, 0x43800000, v84
	v_mul_f32_e32 v6, 0x43800000, v88
	v_med3_f32 v4, v4, s0, v1
	v_med3_f32 v6, v6, s0, v1
	v_mov_b32_e32 v145, v5
	v_cvt_pk_fp8_f32 v145, v4, v6
	v_mul_f32_e32 v7, 0x43800000, v112
	v_mul_f32_e32 v4, 0x43800000, v104
	v_med3_f32 v6, v7, s0, v1
	v_med3_f32 v4, v4, s0, v1
	v_cvt_pk_fp8_f32 v145, v6, v4 op_sel:[0,0,1]
	v_mul_f32_e32 v4, 0x43800000, v9
	v_mul_f32_e32 v6, 0x43800000, v13
	v_med3_f32 v4, v4, s0, v1
	v_med3_f32 v8, v6, s0, v1
	v_mov_b32_e32 v6, v5
	v_cvt_pk_fp8_f32 v6, v4, v8
	v_mul_f32_e32 v7, 0x43800000, v21
	v_mul_f32_e32 v4, 0x43800000, v17
	v_med3_f32 v7, v7, s0, v1
	v_med3_f32 v4, v4, s0, v1
	v_cvt_pk_fp8_f32 v6, v7, v4 op_sel:[0,0,1]
	v_mul_f32_e32 v4, 0x43800000, v25
	v_mul_f32_e32 v7, 0x43800000, v29
	v_med3_f32 v4, v4, s0, v1
	v_med3_f32 v9, v7, s0, v1
	v_mov_b32_e32 v7, v5
	v_cvt_pk_fp8_f32 v7, v4, v9
	v_mul_f32_e32 v8, 0x43800000, v45
	v_mul_f32_e32 v4, 0x43800000, v33
	v_med3_f32 v8, v8, s0, v1
	v_med3_f32 v4, v4, s0, v1
	v_cvt_pk_fp8_f32 v7, v8, v4 op_sel:[0,0,1]
	v_mul_f32_e32 v4, 0x43800000, v49
	v_mul_f32_e32 v8, 0x43800000, v57
	v_med3_f32 v4, v4, s0, v1
	v_med3_f32 v10, v8, s0, v1
	v_mov_b32_e32 v8, v5
	v_cvt_pk_fp8_f32 v8, v4, v10
	v_mul_f32_e32 v9, 0x43800000, v81
	v_mul_f32_e32 v4, 0x43800000, v69
	v_med3_f32 v9, v9, s0, v1
	v_med3_f32 v4, v4, s0, v1
	v_cvt_pk_fp8_f32 v8, v9, v4 op_sel:[0,0,1]
	v_mul_f32_e32 v4, 0x43800000, v85
	v_mul_f32_e32 v9, 0x43800000, v89
	v_med3_f32 v4, v4, s0, v1
	v_med3_f32 v11, v9, s0, v1
	v_mov_b32_e32 v9, v5
	v_cvt_pk_fp8_f32 v9, v4, v11
	v_mul_f32_e32 v10, 0x43800000, v113
	v_mul_f32_e32 v4, 0x43800000, v105
	v_med3_f32 v10, v10, s0, v1
	v_med3_f32 v4, v4, s0, v1
	v_cvt_pk_fp8_f32 v9, v10, v4 op_sel:[0,0,1]
	ds_write_b128 v166, v[134:137] offset:34816
	ds_write_b128 v166, v[138:141] offset:35088
	ds_write_b128 v166, v[142:145] offset:35360
	ds_write_b128 v166, v[6:9] offset:35632
	s_waitcnt lgkmcnt(0)
	s_barrier
	s_mov_b32 s1, 0xc00000
	v_add_co_u32_e32 v6, vcc, s1, v2
	s_mov_b32 s1, 0xc04000
	s_nop 0
	v_addc_co_u32_e32 v7, vcc, 0, v3, vcc
	v_add_co_u32_e32 v10, vcc, s1, v2
	s_mov_b32 s1, 0xc08000
	s_nop 0
	v_addc_co_u32_e32 v11, vcc, 0, v3, vcc
	global_load_dwordx4 v[6:9], v[6:7], off sc0 nt
	s_nop 0
	global_load_dwordx4 v[14:17], v[10:11], off sc0 nt
	v_add_co_u32_e32 v10, vcc, s1, v2
	s_mov_b32 s1, 0xc0c000
	s_nop 0
	v_addc_co_u32_e32 v11, vcc, 0, v3, vcc
	v_add_co_u32_e32 v12, vcc, s1, v2
	s_mov_b32 s1, 0xc10000
	s_nop 0
	v_addc_co_u32_e32 v13, vcc, 0, v3, vcc
	global_load_dwordx4 v[30:33], v[10:11], off sc0 nt
	global_load_dwordx4 v[22:25], v[12:13], off sc0 nt
	v_add_co_u32_e32 v10, vcc, s1, v2
	s_mov_b32 s1, 0xc14000
	s_nop 0
	v_addc_co_u32_e32 v11, vcc, 0, v3, vcc
	v_add_co_u32_e32 v12, vcc, s1, v2
	s_mov_b32 s1, 0xc18000
	s_nop 0
	v_addc_co_u32_e32 v13, vcc, 0, v3, vcc
	global_load_dwordx4 v[42:45], v[10:11], off sc0 nt
	global_load_dwordx4 v[46:49], v[12:13], off sc0 nt
	v_add_co_u32_e32 v10, vcc, s1, v2
	s_mov_b32 s1, 0xc1c000
	s_nop 0
	v_addc_co_u32_e32 v11, vcc, 0, v3, vcc
	v_add_co_u32_e32 v12, vcc, s1, v2
	s_mov_b32 s1, 0xc20000
	s_nop 0
	v_addc_co_u32_e32 v13, vcc, 0, v3, vcc
	global_load_dwordx4 v[66:69], v[10:11], off sc0 nt
	global_load_dwordx4 v[54:57], v[12:13], off sc0 nt
	v_add_co_u32_e32 v10, vcc, s1, v2
	s_mov_b32 s1, 0xc24000
	s_nop 0
	v_addc_co_u32_e32 v11, vcc, 0, v3, vcc
	v_add_co_u32_e32 v12, vcc, s1, v2
	s_mov_b32 s1, 0xc28000
	s_nop 0
	v_addc_co_u32_e32 v13, vcc, 0, v3, vcc
	global_load_dwordx4 v[78:81], v[10:11], off sc0 nt
	global_load_dwordx4 v[82:85], v[12:13], off sc0 nt
	v_add_co_u32_e32 v10, vcc, s1, v2
	s_mov_b32 s1, 0xc2c000
	s_nop 0
	v_addc_co_u32_e32 v11, vcc, 0, v3, vcc
	v_add_co_u32_e32 v12, vcc, s1, v2
	s_mov_b32 s1, 0xc30000
	s_nop 0
	v_addc_co_u32_e32 v13, vcc, 0, v3, vcc
	global_load_dwordx4 v[110:113], v[10:11], off sc0 nt
	global_load_dwordx4 v[102:105], v[12:13], off sc0 nt
	v_add_co_u32_e32 v10, vcc, s1, v2
	s_mov_b32 s1, 0xc34000
	s_nop 0
	v_addc_co_u32_e32 v11, vcc, 0, v3, vcc
	v_add_co_u32_e32 v12, vcc, s1, v2
	s_mov_b32 s1, 0xc38000
	s_nop 0
	v_addc_co_u32_e32 v13, vcc, 0, v3, vcc
	global_load_dwordx4 v[134:137], v[10:11], off sc0 nt
	global_load_dwordx4 v[138:141], v[12:13], off sc0 nt
	v_add_co_u32_e32 v10, vcc, s1, v2
	s_mov_b32 s1, 0xc3c000
	s_nop 0
	v_addc_co_u32_e32 v11, vcc, 0, v3, vcc
	v_add_co_u32_e32 v12, vcc, s1, v2
	s_nop 1
	v_addc_co_u32_e32 v13, vcc, 0, v3, vcc
	global_load_dwordx4 v[146:149], v[10:11], off sc0 nt
	global_load_dwordx4 v[142:145], v[12:13], off sc0 nt
	ds_read_b128 v[10:13], v154 offset:34816
	ds_read_b128 v[18:21], v156 offset:34816
	ds_read_b128 v[26:29], v158 offset:34816
	ds_read_b128 v[86:89], v162 offset:34816
	s_waitcnt lgkmcnt(3)
	global_store_dwordx4 v[150:151], v[10:13], off offset:256 nt
	s_waitcnt lgkmcnt(2)
	global_store_dwordx4 v[152:153], v[18:21], off offset:256 nt
	s_waitcnt lgkmcnt(1)
	global_store_dwordx4 v[160:161], v[26:29], off offset:256 nt
	s_waitcnt lgkmcnt(0)
	global_store_dwordx4 v[164:165], v[86:89], off offset:256 nt
	s_waitcnt vmcnt(39)
	v_mul_f32_e32 v4, 0x43800000, v34
	s_waitcnt vmcnt(38)
	v_mul_f32_e32 v10, 0x43800000, v38
	v_med3_f32 v4, v4, s0, v1
	v_med3_f32 v12, v10, s0, v1
	v_mov_b32_e32 v10, v5
	v_cvt_pk_fp8_f32 v10, v4, v12
	s_waitcnt vmcnt(37)
	v_mul_f32_e32 v11, 0x43800000, v58
	s_waitcnt vmcnt(36)
	v_mul_f32_e32 v4, 0x43800000, v50
	v_med3_f32 v11, v11, s0, v1
	v_med3_f32 v4, v4, s0, v1
	v_cvt_pk_fp8_f32 v10, v11, v4 op_sel:[0,0,1]
	s_waitcnt vmcnt(35)
	v_mul_f32_e32 v4, 0x43800000, v62
	s_waitcnt vmcnt(34)
	v_mul_f32_e32 v11, 0x43800000, v70
	v_med3_f32 v4, v4, s0, v1
	v_med3_f32 v13, v11, s0, v1
	v_mov_b32_e32 v11, v5
	v_cvt_pk_fp8_f32 v11, v4, v13
	s_waitcnt vmcnt(33)
	v_mul_f32_e32 v12, 0x43800000, v90
	s_waitcnt vmcnt(32)
	v_mul_f32_e32 v4, 0x43800000, v74
	v_med3_f32 v12, v12, s0, v1
	v_med3_f32 v4, v4, s0, v1
	v_cvt_pk_fp8_f32 v11, v12, v4 op_sel:[0,0,1]
	s_waitcnt vmcnt(31)
	v_mul_f32_e32 v4, 0x43800000, v94
	s_waitcnt vmcnt(30)
	v_mul_f32_e32 v12, 0x43800000, v98
	v_med3_f32 v4, v4, s0, v1
	v_med3_f32 v18, v12, s0, v1
	v_mov_b32_e32 v12, v5
	v_cvt_pk_fp8_f32 v12, v4, v18
	s_waitcnt vmcnt(29)
	v_mul_f32_e32 v13, 0x43800000, v114
	s_waitcnt vmcnt(28)
	v_mul_f32_e32 v4, 0x43800000, v106
	v_med3_f32 v13, v13, s0, v1
	v_med3_f32 v4, v4, s0, v1
	v_cvt_pk_fp8_f32 v12, v13, v4 op_sel:[0,0,1]
	s_waitcnt vmcnt(27)
	v_mul_f32_e32 v4, 0x43800000, v118
	s_waitcnt vmcnt(26)
	v_mul_f32_e32 v13, 0x43800000, v122
	v_med3_f32 v4, v4, s0, v1
	v_med3_f32 v19, v13, s0, v1
	v_mov_b32_e32 v13, v5
	v_cvt_pk_fp8_f32 v13, v4, v19
	s_waitcnt vmcnt(25)
	v_mul_f32_e32 v18, 0x43800000, v130
	s_waitcnt vmcnt(24)
	v_mul_f32_e32 v4, 0x43800000, v126
	v_med3_f32 v18, v18, s0, v1
	v_med3_f32 v4, v4, s0, v1
	v_cvt_pk_fp8_f32 v13, v18, v4 op_sel:[0,0,1]
	v_mul_f32_e32 v4, 0x43800000, v35
	v_mul_f32_e32 v18, 0x43800000, v39
	v_med3_f32 v4, v4, s0, v1
	v_med3_f32 v20, v18, s0, v1
	v_mov_b32_e32 v18, v5
	v_cvt_pk_fp8_f32 v18, v4, v20
	v_mul_f32_e32 v19, 0x43800000, v59
	v_mul_f32_e32 v4, 0x43800000, v51
	v_med3_f32 v19, v19, s0, v1
	v_med3_f32 v4, v4, s0, v1
	v_cvt_pk_fp8_f32 v18, v19, v4 op_sel:[0,0,1]
	v_mul_f32_e32 v4, 0x43800000, v63
	v_mul_f32_e32 v19, 0x43800000, v71
	v_med3_f32 v4, v4, s0, v1
	v_med3_f32 v21, v19, s0, v1
	v_mov_b32_e32 v19, v5
	v_cvt_pk_fp8_f32 v19, v4, v21
	v_mul_f32_e32 v20, 0x43800000, v91
	v_mul_f32_e32 v4, 0x43800000, v75
	v_med3_f32 v20, v20, s0, v1
	v_med3_f32 v4, v4, s0, v1
	v_cvt_pk_fp8_f32 v19, v20, v4 op_sel:[0,0,1]
	v_mul_f32_e32 v4, 0x43800000, v95
	v_mul_f32_e32 v20, 0x43800000, v99
	v_med3_f32 v4, v4, s0, v1
	v_med3_f32 v26, v20, s0, v1
	v_mov_b32_e32 v20, v5
	v_cvt_pk_fp8_f32 v20, v4, v26
	v_mul_f32_e32 v21, 0x43800000, v115
	v_mul_f32_e32 v4, 0x43800000, v107
	v_med3_f32 v21, v21, s0, v1
	v_med3_f32 v4, v4, s0, v1
	v_cvt_pk_fp8_f32 v20, v21, v4 op_sel:[0,0,1]
	v_mul_f32_e32 v4, 0x43800000, v119
	v_mul_f32_e32 v21, 0x43800000, v123
	v_med3_f32 v4, v4, s0, v1
	v_med3_f32 v27, v21, s0, v1
	v_mov_b32_e32 v21, v5
	v_cvt_pk_fp8_f32 v21, v4, v27
	v_mul_f32_e32 v26, 0x43800000, v131
	v_mul_f32_e32 v4, 0x43800000, v127
	v_med3_f32 v26, v26, s0, v1
	v_med3_f32 v4, v4, s0, v1
	v_cvt_pk_fp8_f32 v21, v26, v4 op_sel:[0,0,1]
	v_mul_f32_e32 v4, 0x43800000, v36
	v_mul_f32_e32 v26, 0x43800000, v40
	v_med3_f32 v4, v4, s0, v1
	v_med3_f32 v28, v26, s0, v1
	v_mov_b32_e32 v26, v5
	v_cvt_pk_fp8_f32 v26, v4, v28
	v_mul_f32_e32 v27, 0x43800000, v60
	v_mul_f32_e32 v4, 0x43800000, v52
	v_med3_f32 v27, v27, s0, v1
	v_med3_f32 v4, v4, s0, v1
	v_cvt_pk_fp8_f32 v26, v27, v4 op_sel:[0,0,1]
	v_mul_f32_e32 v4, 0x43800000, v64
	v_mul_f32_e32 v27, 0x43800000, v72
	v_med3_f32 v4, v4, s0, v1
	v_med3_f32 v29, v27, s0, v1
	v_mov_b32_e32 v27, v5
	v_cvt_pk_fp8_f32 v27, v4, v29
	v_mul_f32_e32 v28, 0x43800000, v92
	v_mul_f32_e32 v4, 0x43800000, v76
	v_med3_f32 v28, v28, s0, v1
	v_med3_f32 v4, v4, s0, v1
	v_cvt_pk_fp8_f32 v27, v28, v4 op_sel:[0,0,1]
	v_mul_f32_e32 v4, 0x43800000, v96
	v_mul_f32_e32 v28, 0x43800000, v100
	v_med3_f32 v4, v4, s0, v1
	v_med3_f32 v34, v28, s0, v1
	v_mov_b32_e32 v28, v5
	v_cvt_pk_fp8_f32 v28, v4, v34
	v_mul_f32_e32 v29, 0x43800000, v116
	v_mul_f32_e32 v4, 0x43800000, v108
	v_med3_f32 v29, v29, s0, v1
	v_med3_f32 v4, v4, s0, v1
	v_cvt_pk_fp8_f32 v28, v29, v4 op_sel:[0,0,1]
	v_mul_f32_e32 v4, 0x43800000, v120
	v_mul_f32_e32 v29, 0x43800000, v124
	v_med3_f32 v4, v4, s0, v1
	v_med3_f32 v35, v29, s0, v1
	v_mov_b32_e32 v29, v5
	v_cvt_pk_fp8_f32 v29, v4, v35
	v_mul_f32_e32 v34, 0x43800000, v132
	v_mul_f32_e32 v4, 0x43800000, v128
	v_med3_f32 v34, v34, s0, v1
	v_med3_f32 v4, v4, s0, v1
	v_cvt_pk_fp8_f32 v29, v34, v4 op_sel:[0,0,1]
	v_mul_f32_e32 v4, 0x43800000, v37
	v_mul_f32_e32 v34, 0x43800000, v41
	v_med3_f32 v4, v4, s0, v1
	v_med3_f32 v36, v34, s0, v1
	v_mov_b32_e32 v34, v5
	v_cvt_pk_fp8_f32 v34, v4, v36
	v_mul_f32_e32 v35, 0x43800000, v61
	v_mul_f32_e32 v4, 0x43800000, v53
	v_med3_f32 v35, v35, s0, v1
	v_med3_f32 v4, v4, s0, v1
	v_cvt_pk_fp8_f32 v34, v35, v4 op_sel:[0,0,1]
	v_mul_f32_e32 v4, 0x43800000, v65
	v_mul_f32_e32 v35, 0x43800000, v73
	v_med3_f32 v4, v4, s0, v1
	v_med3_f32 v37, v35, s0, v1
	v_mov_b32_e32 v35, v5
	v_cvt_pk_fp8_f32 v35, v4, v37
	v_mul_f32_e32 v36, 0x43800000, v93
	v_mul_f32_e32 v4, 0x43800000, v77
	v_med3_f32 v36, v36, s0, v1
	v_med3_f32 v4, v4, s0, v1
	v_cvt_pk_fp8_f32 v35, v36, v4 op_sel:[0,0,1]
	v_mul_f32_e32 v4, 0x43800000, v97
	v_mul_f32_e32 v36, 0x43800000, v101
	v_med3_f32 v4, v4, s0, v1
	v_med3_f32 v38, v36, s0, v1
	v_mov_b32_e32 v36, v5
	v_cvt_pk_fp8_f32 v36, v4, v38
	v_mul_f32_e32 v37, 0x43800000, v117
	v_mul_f32_e32 v4, 0x43800000, v109
	v_med3_f32 v37, v37, s0, v1
	v_med3_f32 v4, v4, s0, v1
	v_cvt_pk_fp8_f32 v36, v37, v4 op_sel:[0,0,1]
	v_mul_f32_e32 v4, 0x43800000, v121
	v_mul_f32_e32 v37, 0x43800000, v125
	v_med3_f32 v4, v4, s0, v1
	v_med3_f32 v39, v37, s0, v1
	v_mov_b32_e32 v37, v5
	v_cvt_pk_fp8_f32 v37, v4, v39
	v_mul_f32_e32 v38, 0x43800000, v133
	v_mul_f32_e32 v4, 0x43800000, v129
	v_med3_f32 v38, v38, s0, v1
	v_med3_f32 v4, v4, s0, v1
	v_cvt_pk_fp8_f32 v37, v38, v4 op_sel:[0,0,1]
	ds_write_b128 v166, v[10:13]
	ds_write_b128 v166, v[18:21] offset:272
	ds_write_b128 v166, v[26:29] offset:544
	ds_write_b128 v166, v[34:37] offset:816
	s_waitcnt lgkmcnt(0)
	s_barrier
	s_mov_b32 s1, 0x1000000
	v_add_co_u32_e32 v10, vcc, s1, v2
	s_mov_b32 s1, 0x1004000
	s_nop 0
	v_addc_co_u32_e32 v11, vcc, 0, v3, vcc
	v_add_co_u32_e32 v18, vcc, s1, v2
	s_mov_b32 s1, 0x1008000
	s_nop 0
	v_addc_co_u32_e32 v19, vcc, 0, v3, vcc
	v_add_co_u32_e32 v38, vcc, s1, v2
	s_mov_b32 s1, 0x100c000
	s_nop 0
	v_addc_co_u32_e32 v39, vcc, 0, v3, vcc
	v_add_co_u32_e32 v40, vcc, s1, v2
	s_mov_b32 s1, 0x1010000
	s_nop 0
	v_addc_co_u32_e32 v41, vcc, 0, v3, vcc
	v_add_co_u32_e32 v58, vcc, s1, v2
	s_mov_b32 s1, 0x1014000
	s_nop 0
	v_addc_co_u32_e32 v59, vcc, 0, v3, vcc
	v_add_co_u32_e32 v60, vcc, s1, v2
	s_mov_b32 s1, 0x1018000
	s_nop 0
	v_addc_co_u32_e32 v61, vcc, 0, v3, vcc
	v_add_co_u32_e32 v70, vcc, s1, v2
	s_mov_b32 s1, 0x101c000
	s_nop 0
	v_addc_co_u32_e32 v71, vcc, 0, v3, vcc
	v_add_co_u32_e32 v72, vcc, s1, v2
	s_mov_b32 s1, 0x1020000
	s_nop 0
	v_addc_co_u32_e32 v73, vcc, 0, v3, vcc
	v_add_co_u32_e32 v74, vcc, s1, v2
	s_mov_b32 s1, 0x1024000
	s_nop 0
	v_addc_co_u32_e32 v75, vcc, 0, v3, vcc
	v_add_co_u32_e32 v76, vcc, s1, v2
	s_mov_b32 s1, 0x1028000
	s_nop 0
	v_addc_co_u32_e32 v77, vcc, 0, v3, vcc
	global_load_dwordx4 v[10:13], v[10:11], off sc0 nt
	s_nop 0
	global_load_dwordx4 v[18:21], v[18:19], off sc0 nt
	s_nop 0
	global_load_dwordx4 v[34:37], v[38:39], off sc0 nt
	global_load_dwordx4 v[26:29], v[40:41], off sc0 nt
	s_nop 0
	global_load_dwordx4 v[38:41], v[58:59], off sc0 nt
	global_load_dwordx4 v[50:53], v[60:61], off sc0 nt
	global_load_dwordx4 v[62:65], v[70:71], off sc0 nt
	s_nop 0
	global_load_dwordx4 v[58:61], v[72:73], off sc0 nt
	s_nop 0
	global_load_dwordx4 v[70:73], v[74:75], off sc0 nt
	global_load_dwordx4 v[86:89], v[76:77], off sc0 nt
	v_add_co_u32_e32 v74, vcc, s1, v2
	s_mov_b32 s1, 0x102c000
	s_nop 0
	v_addc_co_u32_e32 v75, vcc, 0, v3, vcc
	v_add_co_u32_e32 v76, vcc, s1, v2
	s_mov_b32 s1, 0x1030000
	s_nop 0
	v_addc_co_u32_e32 v77, vcc, 0, v3, vcc
	global_load_dwordx4 v[98:101], v[74:75], off sc0 nt
	global_load_dwordx4 v[90:93], v[76:77], off sc0 nt
	v_add_co_u32_e32 v74, vcc, s1, v2
	s_mov_b32 s1, 0x1034000
	s_nop 0
	v_addc_co_u32_e32 v75, vcc, 0, v3, vcc
	v_add_co_u32_e32 v76, vcc, s1, v2
	s_mov_b32 s1, 0x1038000
	s_nop 0
	v_addc_co_u32_e32 v77, vcc, 0, v3, vcc
	global_load_dwordx4 v[106:109], v[74:75], off sc0 nt
	global_load_dwordx4 v[114:117], v[76:77], off sc0 nt
	v_add_co_u32_e32 v74, vcc, s1, v2
	s_mov_b32 s1, 0x103c000
	s_nop 0
	v_addc_co_u32_e32 v75, vcc, 0, v3, vcc
	v_add_co_u32_e32 v76, vcc, s1, v2
	s_nop 1
	v_addc_co_u32_e32 v77, vcc, 0, v3, vcc
	global_load_dwordx4 v[130:133], v[74:75], off sc0 nt
	global_load_dwordx4 v[122:125], v[76:77], off sc0 nt
	ds_read_b128 v[74:77], v154
	ds_read_b128 v[94:97], v156
	ds_read_b128 v[118:121], v158
	ds_read_b128 v[126:129], v162
	s_waitcnt lgkmcnt(3)
	global_store_dwordx4 v[150:151], v[74:77], off offset:512 nt
	s_waitcnt lgkmcnt(2)
	global_store_dwordx4 v[152:153], v[94:97], off offset:512 nt
	s_waitcnt lgkmcnt(1)
	global_store_dwordx4 v[160:161], v[118:121], off offset:512 nt
	s_waitcnt lgkmcnt(0)
	global_store_dwordx4 v[164:165], v[126:129], off offset:512 nt
	s_waitcnt vmcnt(39)
	v_mul_f32_e32 v4, 0x43800000, v6
	s_waitcnt vmcnt(38)
	v_mul_f32_e32 v6, 0x43800000, v14
	v_med3_f32 v4, v4, s0, v1
	v_med3_f32 v6, v6, s0, v1
	v_mov_b32_e32 v74, v5
	v_cvt_pk_fp8_f32 v74, v4, v6
	s_waitcnt vmcnt(37)
	v_mul_f32_e32 v14, 0x43800000, v30
	s_waitcnt vmcnt(36)
	v_mul_f32_e32 v4, 0x43800000, v22
	v_med3_f32 v6, v14, s0, v1
	v_med3_f32 v4, v4, s0, v1
	v_cvt_pk_fp8_f32 v74, v6, v4 op_sel:[0,0,1]
	s_waitcnt vmcnt(35)
	v_mul_f32_e32 v4, 0x43800000, v42
	s_waitcnt vmcnt(34)
	v_mul_f32_e32 v6, 0x43800000, v46
	v_med3_f32 v4, v4, s0, v1
	v_med3_f32 v6, v6, s0, v1
	v_mov_b32_e32 v75, v5
	v_cvt_pk_fp8_f32 v75, v4, v6
	s_waitcnt vmcnt(33)
	v_mul_f32_e32 v14, 0x43800000, v66
	s_waitcnt vmcnt(32)
	v_mul_f32_e32 v4, 0x43800000, v54
	v_med3_f32 v6, v14, s0, v1
	v_med3_f32 v4, v4, s0, v1
	v_cvt_pk_fp8_f32 v75, v6, v4 op_sel:[0,0,1]
	s_waitcnt vmcnt(31)
	v_mul_f32_e32 v4, 0x43800000, v78
	s_waitcnt vmcnt(30)
	v_mul_f32_e32 v6, 0x43800000, v82
	v_med3_f32 v4, v4, s0, v1
	v_med3_f32 v6, v6, s0, v1
	v_mov_b32_e32 v76, v5
	v_cvt_pk_fp8_f32 v76, v4, v6
	s_waitcnt vmcnt(29)
	v_mul_f32_e32 v14, 0x43800000, v110
	s_waitcnt vmcnt(28)
	v_mul_f32_e32 v4, 0x43800000, v102
	v_med3_f32 v6, v14, s0, v1
	v_med3_f32 v4, v4, s0, v1
	v_cvt_pk_fp8_f32 v76, v6, v4 op_sel:[0,0,1]
	s_waitcnt vmcnt(27)
	v_mul_f32_e32 v4, 0x43800000, v134
	s_waitcnt vmcnt(26)
	v_mul_f32_e32 v6, 0x43800000, v138
	v_med3_f32 v4, v4, s0, v1
	v_med3_f32 v6, v6, s0, v1
	v_mov_b32_e32 v77, v5
	v_cvt_pk_fp8_f32 v77, v4, v6
	s_waitcnt vmcnt(25)
	v_mul_f32_e32 v14, 0x43800000, v146
	s_waitcnt vmcnt(24)
	v_mul_f32_e32 v4, 0x43800000, v142
	v_med3_f32 v6, v14, s0, v1
	v_med3_f32 v4, v4, s0, v1
	v_cvt_pk_fp8_f32 v77, v6, v4 op_sel:[0,0,1]
	v_mul_f32_e32 v4, 0x43800000, v7
	v_mul_f32_e32 v6, 0x43800000, v15
	v_med3_f32 v4, v4, s0, v1
	v_med3_f32 v6, v6, s0, v1
	v_mov_b32_e32 v94, v5
	v_cvt_pk_fp8_f32 v94, v4, v6
	v_mul_f32_e32 v7, 0x43800000, v31
	v_mul_f32_e32 v4, 0x43800000, v23
	v_med3_f32 v6, v7, s0, v1
	v_med3_f32 v4, v4, s0, v1
	v_cvt_pk_fp8_f32 v94, v6, v4 op_sel:[0,0,1]
	v_mul_f32_e32 v4, 0x43800000, v43
	v_mul_f32_e32 v6, 0x43800000, v47
	v_med3_f32 v4, v4, s0, v1
	v_med3_f32 v6, v6, s0, v1
	v_mov_b32_e32 v95, v5
	v_cvt_pk_fp8_f32 v95, v4, v6
	v_mul_f32_e32 v7, 0x43800000, v67
	v_mul_f32_e32 v4, 0x43800000, v55
	v_med3_f32 v6, v7, s0, v1
	v_med3_f32 v4, v4, s0, v1
	v_cvt_pk_fp8_f32 v95, v6, v4 op_sel:[0,0,1]
	v_mul_f32_e32 v4, 0x43800000, v79
	v_mul_f32_e32 v6, 0x43800000, v83
	v_med3_f32 v4, v4, s0, v1
	v_med3_f32 v6, v6, s0, v1
	v_mov_b32_e32 v96, v5
	v_cvt_pk_fp8_f32 v96, v4, v6
	v_mul_f32_e32 v7, 0x43800000, v111
	v_mul_f32_e32 v4, 0x43800000, v103
	v_med3_f32 v6, v7, s0, v1
	v_med3_f32 v4, v4, s0, v1
	v_cvt_pk_fp8_f32 v96, v6, v4 op_sel:[0,0,1]
	v_mul_f32_e32 v4, 0x43800000, v135
	v_mul_f32_e32 v6, 0x43800000, v139
	v_med3_f32 v4, v4, s0, v1
	v_med3_f32 v6, v6, s0, v1
	v_mov_b32_e32 v97, v5
	v_cvt_pk_fp8_f32 v97, v4, v6
	v_mul_f32_e32 v7, 0x43800000, v147
	v_mul_f32_e32 v4, 0x43800000, v143
	v_med3_f32 v6, v7, s0, v1
	v_med3_f32 v4, v4, s0, v1
	v_cvt_pk_fp8_f32 v97, v6, v4 op_sel:[0,0,1]
	v_mul_f32_e32 v4, 0x43800000, v8
	v_mul_f32_e32 v6, 0x43800000, v16
	v_med3_f32 v4, v4, s0, v1
	v_med3_f32 v6, v6, s0, v1
	v_mov_b32_e32 v118, v5
	v_cvt_pk_fp8_f32 v118, v4, v6
	v_mul_f32_e32 v7, 0x43800000, v32
	v_mul_f32_e32 v4, 0x43800000, v24
	v_med3_f32 v6, v7, s0, v1
	v_med3_f32 v4, v4, s0, v1
	v_cvt_pk_fp8_f32 v118, v6, v4 op_sel:[0,0,1]
	v_mul_f32_e32 v4, 0x43800000, v44
	v_mul_f32_e32 v6, 0x43800000, v48
	v_med3_f32 v4, v4, s0, v1
	v_med3_f32 v6, v6, s0, v1
	v_mov_b32_e32 v119, v5
	v_cvt_pk_fp8_f32 v119, v4, v6
	v_mul_f32_e32 v7, 0x43800000, v68
	v_mul_f32_e32 v4, 0x43800000, v56
	v_med3_f32 v6, v7, s0, v1
	v_med3_f32 v4, v4, s0, v1
	v_cvt_pk_fp8_f32 v119, v6, v4 op_sel:[0,0,1]
	v_mul_f32_e32 v4, 0x43800000, v80
	v_mul_f32_e32 v6, 0x43800000, v84
	v_med3_f32 v4, v4, s0, v1
	v_med3_f32 v6, v6, s0, v1
	v_mov_b32_e32 v120, v5
	v_cvt_pk_fp8_f32 v120, v4, v6
	v_mul_f32_e32 v7, 0x43800000, v112
	v_mul_f32_e32 v4, 0x43800000, v104
	v_med3_f32 v6, v7, s0, v1
	v_med3_f32 v4, v4, s0, v1
	v_cvt_pk_fp8_f32 v120, v6, v4 op_sel:[0,0,1]
	v_mul_f32_e32 v4, 0x43800000, v136
	v_mul_f32_e32 v6, 0x43800000, v140
	v_med3_f32 v4, v4, s0, v1
	v_med3_f32 v6, v6, s0, v1
	v_mov_b32_e32 v121, v5
	v_cvt_pk_fp8_f32 v121, v4, v6
	v_mul_f32_e32 v7, 0x43800000, v148
	v_mul_f32_e32 v4, 0x43800000, v144
	v_med3_f32 v6, v7, s0, v1
	v_med3_f32 v4, v4, s0, v1
	v_cvt_pk_fp8_f32 v121, v6, v4 op_sel:[0,0,1]
	v_mul_f32_e32 v4, 0x43800000, v9
	v_mul_f32_e32 v6, 0x43800000, v17
	v_med3_f32 v4, v4, s0, v1
	v_med3_f32 v8, v6, s0, v1
	v_mov_b32_e32 v6, v5
	v_cvt_pk_fp8_f32 v6, v4, v8
	v_mul_f32_e32 v7, 0x43800000, v33
	v_mul_f32_e32 v4, 0x43800000, v25
	v_med3_f32 v7, v7, s0, v1
	v_med3_f32 v4, v4, s0, v1
	v_cvt_pk_fp8_f32 v6, v7, v4 op_sel:[0,0,1]
	v_mul_f32_e32 v4, 0x43800000, v45
	v_mul_f32_e32 v7, 0x43800000, v49
	v_med3_f32 v4, v4, s0, v1
	v_med3_f32 v9, v7, s0, v1
	v_mov_b32_e32 v7, v5
	v_cvt_pk_fp8_f32 v7, v4, v9
	v_mul_f32_e32 v8, 0x43800000, v69
	v_mul_f32_e32 v4, 0x43800000, v57
	v_med3_f32 v8, v8, s0, v1
	v_med3_f32 v4, v4, s0, v1
	v_cvt_pk_fp8_f32 v7, v8, v4 op_sel:[0,0,1]
	v_mul_f32_e32 v4, 0x43800000, v81
	v_mul_f32_e32 v8, 0x43800000, v85
	v_med3_f32 v4, v4, s0, v1
	v_med3_f32 v14, v8, s0, v1
	v_mov_b32_e32 v8, v5
	v_cvt_pk_fp8_f32 v8, v4, v14
	v_mul_f32_e32 v9, 0x43800000, v113
	v_mul_f32_e32 v4, 0x43800000, v105
	v_med3_f32 v9, v9, s0, v1
	v_med3_f32 v4, v4, s0, v1
	v_cvt_pk_fp8_f32 v8, v9, v4 op_sel:[0,0,1]
	v_mul_f32_e32 v4, 0x43800000, v137
	v_mul_f32_e32 v9, 0x43800000, v141
	v_med3_f32 v4, v4, s0, v1
	v_med3_f32 v15, v9, s0, v1
	v_mov_b32_e32 v9, v5
	v_cvt_pk_fp8_f32 v9, v4, v15
	v_mul_f32_e32 v14, 0x43800000, v149
	v_mul_f32_e32 v4, 0x43800000, v145
	v_med3_f32 v14, v14, s0, v1
	v_med3_f32 v4, v4, s0, v1
	v_cvt_pk_fp8_f32 v9, v14, v4 op_sel:[0,0,1]
	ds_write_b128 v166, v[74:77] offset:34816
	ds_write_b128 v166, v[94:97] offset:35088
	ds_write_b128 v166, v[118:121] offset:35360
	ds_write_b128 v166, v[6:9] offset:35632
	s_waitcnt lgkmcnt(0)
	s_barrier
	s_mov_b32 s1, 0x1400000
	v_add_co_u32_e32 v6, vcc, s1, v2
	s_mov_b32 s1, 0x1404000
	s_nop 0
	v_addc_co_u32_e32 v7, vcc, 0, v3, vcc
	v_add_co_u32_e32 v14, vcc, s1, v2
	s_mov_b32 s1, 0x1408000
	s_nop 0
	v_addc_co_u32_e32 v15, vcc, 0, v3, vcc
	v_add_co_u32_e32 v42, vcc, s1, v2
	s_mov_b32 s1, 0x140c000
	s_nop 0
	v_addc_co_u32_e32 v43, vcc, 0, v3, vcc
	v_add_co_u32_e32 v44, vcc, s1, v2
	s_mov_b32 s1, 0x1410000
	s_nop 0
	v_addc_co_u32_e32 v45, vcc, 0, v3, vcc
	v_add_co_u32_e32 v54, vcc, s1, v2
	s_mov_b32 s1, 0x1414000
	s_nop 0
	v_addc_co_u32_e32 v55, vcc, 0, v3, vcc
	v_add_co_u32_e32 v56, vcc, s1, v2
	s_mov_b32 s1, 0x1418000
	s_nop 0
	v_addc_co_u32_e32 v57, vcc, 0, v3, vcc
	v_add_co_u32_e32 v74, vcc, s1, v2
	s_mov_b32 s1, 0x141c000
	s_nop 0
	v_addc_co_u32_e32 v75, vcc, 0, v3, vcc
	v_add_co_u32_e32 v76, vcc, s1, v2
	s_mov_b32 s1, 0x1420000
	s_nop 0
	v_addc_co_u32_e32 v77, vcc, 0, v3, vcc
	v_add_co_u32_e32 v82, vcc, s1, v2
	s_mov_b32 s1, 0x1424000
	s_nop 0
	v_addc_co_u32_e32 v83, vcc, 0, v3, vcc
	v_add_co_u32_e32 v84, vcc, s1, v2
	s_mov_b32 s1, 0x1428000
	s_nop 0
	v_addc_co_u32_e32 v85, vcc, 0, v3, vcc
	global_load_dwordx4 v[6:9], v[6:7], off sc0 nt
	s_nop 0
	global_load_dwordx4 v[14:17], v[14:15], off sc0 nt
	s_nop 0
	global_load_dwordx4 v[30:33], v[42:43], off sc0 nt
	global_load_dwordx4 v[22:25], v[44:45], off sc0 nt
	s_nop 0
	global_load_dwordx4 v[42:45], v[54:55], off sc0 nt
	global_load_dwordx4 v[46:49], v[56:57], off sc0 nt
	global_load_dwordx4 v[66:69], v[74:75], off sc0 nt
	s_nop 0
	global_load_dwordx4 v[54:57], v[76:77], off sc0 nt
	s_nop 0
	global_load_dwordx4 v[74:77], v[82:83], off sc0 nt
	global_load_dwordx4 v[78:81], v[84:85], off sc0 nt
	v_add_co_u32_e32 v82, vcc, s1, v2
	s_mov_b32 s1, 0x142c000
	s_nop 0
	v_addc_co_u32_e32 v83, vcc, 0, v3, vcc
	v_add_co_u32_e32 v84, vcc, s1, v2
	s_mov_b32 s1, 0x1430000
	s_nop 0
	v_addc_co_u32_e32 v85, vcc, 0, v3, vcc
	global_load_dwordx4 v[102:105], v[82:83], off sc0 nt
	global_load_dwordx4 v[94:97], v[84:85], off sc0 nt
	v_add_co_u32_e32 v82, vcc, s1, v2
	s_mov_b32 s1, 0x1434000
	s_nop 0
	v_addc_co_u32_e32 v83, vcc, 0, v3, vcc
	v_add_co_u32_e32 v84, vcc, s1, v2
	s_mov_b32 s1, 0x1438000
	s_nop 0
	v_addc_co_u32_e32 v85, vcc, 0, v3, vcc
	global_load_dwordx4 v[110:113], v[82:83], off sc0 nt
	global_load_dwordx4 v[118:121], v[84:85], off sc0 nt
	v_add_co_u32_e32 v82, vcc, s1, v2
	s_mov_b32 s1, 0x143c000
	s_nop 0
	v_addc_co_u32_e32 v83, vcc, 0, v3, vcc
	v_add_co_u32_e32 v84, vcc, s1, v2
	s_nop 1
	v_addc_co_u32_e32 v85, vcc, 0, v3, vcc
	global_load_dwordx4 v[134:137], v[82:83], off sc0 nt
	global_load_dwordx4 v[126:129], v[84:85], off sc0 nt
	ds_read_b128 v[82:85], v154 offset:34816
	ds_read_b128 v[138:141], v156 offset:34816
	ds_read_b128 v[142:145], v158 offset:34816
	ds_read_b128 v[146:149], v162 offset:34816
	s_waitcnt lgkmcnt(3)
	global_store_dwordx4 v[150:151], v[82:85], off offset:768 nt
	s_waitcnt lgkmcnt(2)
	global_store_dwordx4 v[152:153], v[138:141], off offset:768 nt
	s_waitcnt lgkmcnt(1)
	global_store_dwordx4 v[160:161], v[142:145], off offset:768 nt
	s_waitcnt lgkmcnt(0)
	global_store_dwordx4 v[164:165], v[146:149], off offset:768 nt
	s_waitcnt vmcnt(39)
	v_mul_f32_e32 v4, 0x43800000, v10
	s_waitcnt vmcnt(38)
	v_mul_f32_e32 v10, 0x43800000, v18
	v_med3_f32 v4, v4, s0, v1
	v_med3_f32 v10, v10, s0, v1
	v_mov_b32_e32 v82, v5
	v_cvt_pk_fp8_f32 v82, v4, v10
	s_waitcnt vmcnt(37)
	v_mul_f32_e32 v18, 0x43800000, v34
	s_waitcnt vmcnt(36)
	v_mul_f32_e32 v4, 0x43800000, v26
	v_med3_f32 v10, v18, s0, v1
	v_med3_f32 v4, v4, s0, v1
	v_cvt_pk_fp8_f32 v82, v10, v4 op_sel:[0,0,1]
	s_waitcnt vmcnt(35)
	v_mul_f32_e32 v4, 0x43800000, v38
	s_waitcnt vmcnt(34)
	v_mul_f32_e32 v10, 0x43800000, v50
	v_med3_f32 v4, v4, s0, v1
	v_med3_f32 v10, v10, s0, v1
	v_mov_b32_e32 v83, v5
	v_cvt_pk_fp8_f32 v83, v4, v10
	s_waitcnt vmcnt(33)
	v_mul_f32_e32 v18, 0x43800000, v62
	s_waitcnt vmcnt(32)
	v_mul_f32_e32 v4, 0x43800000, v58
	v_med3_f32 v10, v18, s0, v1
	v_med3_f32 v4, v4, s0, v1
	v_cvt_pk_fp8_f32 v83, v10, v4 op_sel:[0,0,1]
	s_waitcnt vmcnt(31)
	v_mul_f32_e32 v4, 0x43800000, v70
	s_waitcnt vmcnt(30)
	v_mul_f32_e32 v10, 0x43800000, v86
	v_med3_f32 v4, v4, s0, v1
	v_med3_f32 v10, v10, s0, v1
	v_mov_b32_e32 v84, v5
	v_cvt_pk_fp8_f32 v84, v4, v10
	s_waitcnt vmcnt(29)
	v_mul_f32_e32 v18, 0x43800000, v98
	s_waitcnt vmcnt(28)
	v_mul_f32_e32 v4, 0x43800000, v90
	v_med3_f32 v10, v18, s0, v1
	v_med3_f32 v4, v4, s0, v1
	v_cvt_pk_fp8_f32 v84, v10, v4 op_sel:[0,0,1]
	s_waitcnt vmcnt(27)
	v_mul_f32_e32 v4, 0x43800000, v106
	s_waitcnt vmcnt(26)
	v_mul_f32_e32 v10, 0x43800000, v114
	v_med3_f32 v4, v4, s0, v1
	v_med3_f32 v10, v10, s0, v1
	v_mov_b32_e32 v85, v5
	v_cvt_pk_fp8_f32 v85, v4, v10
	s_waitcnt vmcnt(25)
	v_mul_f32_e32 v18, 0x43800000, v130
	s_waitcnt vmcnt(24)
	v_mul_f32_e32 v4, 0x43800000, v122
	v_med3_f32 v10, v18, s0, v1
	v_med3_f32 v4, v4, s0, v1
	v_cvt_pk_fp8_f32 v85, v10, v4 op_sel:[0,0,1]
	v_mul_f32_e32 v4, 0x43800000, v11
	v_mul_f32_e32 v10, 0x43800000, v19
	v_med3_f32 v4, v4, s0, v1
	v_med3_f32 v10, v10, s0, v1
	v_mov_b32_e32 v138, v5
	v_cvt_pk_fp8_f32 v138, v4, v10
	v_mul_f32_e32 v11, 0x43800000, v35
	v_mul_f32_e32 v4, 0x43800000, v27
	v_med3_f32 v10, v11, s0, v1
	v_med3_f32 v4, v4, s0, v1
	v_cvt_pk_fp8_f32 v138, v10, v4 op_sel:[0,0,1]
	v_mul_f32_e32 v4, 0x43800000, v39
	v_mul_f32_e32 v10, 0x43800000, v51
	v_med3_f32 v4, v4, s0, v1
	v_med3_f32 v10, v10, s0, v1
	v_mov_b32_e32 v139, v5
	v_cvt_pk_fp8_f32 v139, v4, v10
	v_mul_f32_e32 v11, 0x43800000, v63
	v_mul_f32_e32 v4, 0x43800000, v59
	v_med3_f32 v10, v11, s0, v1
	v_med3_f32 v4, v4, s0, v1
	v_cvt_pk_fp8_f32 v139, v10, v4 op_sel:[0,0,1]
	v_mul_f32_e32 v4, 0x43800000, v71
	v_mul_f32_e32 v10, 0x43800000, v87
	v_med3_f32 v4, v4, s0, v1
	v_med3_f32 v10, v10, s0, v1
	v_mov_b32_e32 v140, v5
	v_cvt_pk_fp8_f32 v140, v4, v10
	v_mul_f32_e32 v11, 0x43800000, v99
	v_mul_f32_e32 v4, 0x43800000, v91
	v_med3_f32 v10, v11, s0, v1
	v_med3_f32 v4, v4, s0, v1
	v_cvt_pk_fp8_f32 v140, v10, v4 op_sel:[0,0,1]
	v_mul_f32_e32 v4, 0x43800000, v107
	v_mul_f32_e32 v10, 0x43800000, v115
	v_med3_f32 v4, v4, s0, v1
	v_med3_f32 v10, v10, s0, v1
	v_mov_b32_e32 v141, v5
	v_cvt_pk_fp8_f32 v141, v4, v10
	v_mul_f32_e32 v11, 0x43800000, v131
	v_mul_f32_e32 v4, 0x43800000, v123
	v_med3_f32 v10, v11, s0, v1
	v_med3_f32 v4, v4, s0, v1
	v_cvt_pk_fp8_f32 v141, v10, v4 op_sel:[0,0,1]
	v_mul_f32_e32 v4, 0x43800000, v12
	v_mul_f32_e32 v10, 0x43800000, v20
	v_med3_f32 v4, v4, s0, v1
	v_med3_f32 v10, v10, s0, v1
	v_mov_b32_e32 v142, v5
	v_cvt_pk_fp8_f32 v142, v4, v10
	v_mul_f32_e32 v11, 0x43800000, v36
	v_mul_f32_e32 v4, 0x43800000, v28
	v_med3_f32 v10, v11, s0, v1
	v_med3_f32 v4, v4, s0, v1
	v_cvt_pk_fp8_f32 v142, v10, v4 op_sel:[0,0,1]
	v_mul_f32_e32 v4, 0x43800000, v40
	v_mul_f32_e32 v10, 0x43800000, v52
	v_med3_f32 v4, v4, s0, v1
	v_med3_f32 v10, v10, s0, v1
	v_mov_b32_e32 v143, v5
	v_cvt_pk_fp8_f32 v143, v4, v10
	v_mul_f32_e32 v11, 0x43800000, v64
	v_mul_f32_e32 v4, 0x43800000, v60
	v_med3_f32 v10, v11, s0, v1
	v_med3_f32 v4, v4, s0, v1
	v_cvt_pk_fp8_f32 v143, v10, v4 op_sel:[0,0,1]
	v_mul_f32_e32 v4, 0x43800000, v72
	v_mul_f32_e32 v10, 0x43800000, v88
	v_med3_f32 v4, v4, s0, v1
	v_med3_f32 v10, v10, s0, v1
	v_mov_b32_e32 v144, v5
	v_cvt_pk_fp8_f32 v144, v4, v10
	v_mul_f32_e32 v11, 0x43800000, v100
	v_mul_f32_e32 v4, 0x43800000, v92
	v_med3_f32 v10, v11, s0, v1
	v_med3_f32 v4, v4, s0, v1
	v_cvt_pk_fp8_f32 v144, v10, v4 op_sel:[0,0,1]
	v_mul_f32_e32 v4, 0x43800000, v108
	v_mul_f32_e32 v10, 0x43800000, v116
	v_med3_f32 v4, v4, s0, v1
	v_med3_f32 v10, v10, s0, v1
	v_mov_b32_e32 v145, v5
	v_cvt_pk_fp8_f32 v145, v4, v10
	v_mul_f32_e32 v11, 0x43800000, v132
	v_mul_f32_e32 v4, 0x43800000, v124
	v_med3_f32 v10, v11, s0, v1
	v_med3_f32 v4, v4, s0, v1
	v_cvt_pk_fp8_f32 v145, v10, v4 op_sel:[0,0,1]
	v_mul_f32_e32 v4, 0x43800000, v13
	v_mul_f32_e32 v10, 0x43800000, v21
	v_med3_f32 v4, v4, s0, v1
	v_med3_f32 v12, v10, s0, v1
	v_mov_b32_e32 v10, v5
	v_cvt_pk_fp8_f32 v10, v4, v12
	v_mul_f32_e32 v11, 0x43800000, v37
	v_mul_f32_e32 v4, 0x43800000, v29
	v_med3_f32 v11, v11, s0, v1
	v_med3_f32 v4, v4, s0, v1
	v_cvt_pk_fp8_f32 v10, v11, v4 op_sel:[0,0,1]
	v_mul_f32_e32 v4, 0x43800000, v41
	v_mul_f32_e32 v11, 0x43800000, v53
	v_med3_f32 v4, v4, s0, v1
	v_med3_f32 v13, v11, s0, v1
	v_mov_b32_e32 v11, v5
	v_cvt_pk_fp8_f32 v11, v4, v13
	v_mul_f32_e32 v12, 0x43800000, v65
	v_mul_f32_e32 v4, 0x43800000, v61
	v_med3_f32 v12, v12, s0, v1
	v_med3_f32 v4, v4, s0, v1
	v_cvt_pk_fp8_f32 v11, v12, v4 op_sel:[0,0,1]
	v_mul_f32_e32 v4, 0x43800000, v73
	v_mul_f32_e32 v12, 0x43800000, v89
	v_med3_f32 v4, v4, s0, v1
	v_med3_f32 v18, v12, s0, v1
	v_mov_b32_e32 v12, v5
	v_cvt_pk_fp8_f32 v12, v4, v18
	v_mul_f32_e32 v13, 0x43800000, v101
	v_mul_f32_e32 v4, 0x43800000, v93
	v_med3_f32 v13, v13, s0, v1
	v_med3_f32 v4, v4, s0, v1
	v_cvt_pk_fp8_f32 v12, v13, v4 op_sel:[0,0,1]
	v_mul_f32_e32 v4, 0x43800000, v109
	v_mul_f32_e32 v13, 0x43800000, v117
	v_med3_f32 v4, v4, s0, v1
	v_med3_f32 v19, v13, s0, v1
	v_mov_b32_e32 v13, v5
	v_cvt_pk_fp8_f32 v13, v4, v19
	v_mul_f32_e32 v18, 0x43800000, v133
	v_mul_f32_e32 v4, 0x43800000, v125
	v_med3_f32 v18, v18, s0, v1
	v_med3_f32 v4, v4, s0, v1
	v_cvt_pk_fp8_f32 v13, v18, v4 op_sel:[0,0,1]
	ds_write_b128 v166, v[82:85]
	ds_write_b128 v166, v[138:141] offset:272
	ds_write_b128 v166, v[142:145] offset:544
	ds_write_b128 v166, v[10:13] offset:816
	s_waitcnt lgkmcnt(0)
	s_barrier
	s_mov_b32 s1, 0x1800000
	v_add_co_u32_e32 v10, vcc, s1, v2
	s_mov_b32 s1, 0x1804000
	s_nop 0
	v_addc_co_u32_e32 v11, vcc, 0, v3, vcc
	v_add_co_u32_e32 v18, vcc, s1, v2
	s_mov_b32 s1, 0x1808000
	s_nop 0
	v_addc_co_u32_e32 v19, vcc, 0, v3, vcc
	v_add_co_u32_e32 v38, vcc, s1, v2
	s_mov_b32 s1, 0x180c000
	s_nop 0
	v_addc_co_u32_e32 v39, vcc, 0, v3, vcc
	v_add_co_u32_e32 v40, vcc, s1, v2
	s_mov_b32 s1, 0x1810000
	s_nop 0
	v_addc_co_u32_e32 v41, vcc, 0, v3, vcc
	v_add_co_u32_e32 v58, vcc, s1, v2
	s_mov_b32 s1, 0x1814000
	s_nop 0
	v_addc_co_u32_e32 v59, vcc, 0, v3, vcc
	v_add_co_u32_e32 v60, vcc, s1, v2
	s_mov_b32 s1, 0x1818000
	s_nop 0
	v_addc_co_u32_e32 v61, vcc, 0, v3, vcc
	v_add_co_u32_e32 v70, vcc, s1, v2
	s_mov_b32 s1, 0x181c000
	s_nop 0
	v_addc_co_u32_e32 v71, vcc, 0, v3, vcc
	v_add_co_u32_e32 v72, vcc, s1, v2
	s_mov_b32 s1, 0x1820000
	s_nop 0
	v_addc_co_u32_e32 v73, vcc, 0, v3, vcc
	v_add_co_u32_e32 v86, vcc, s1, v2
	s_mov_b32 s1, 0x1824000
	s_nop 0
	v_addc_co_u32_e32 v87, vcc, 0, v3, vcc
	v_add_co_u32_e32 v88, vcc, s1, v2
	s_mov_b32 s1, 0x1828000
	s_nop 0
	v_addc_co_u32_e32 v89, vcc, 0, v3, vcc
	global_load_dwordx4 v[10:13], v[10:11], off sc0 nt
	s_nop 0
	global_load_dwordx4 v[18:21], v[18:19], off sc0 nt
	s_nop 0
	global_load_dwordx4 v[34:37], v[38:39], off sc0 nt
	global_load_dwordx4 v[26:29], v[40:41], off sc0 nt
	s_nop 0
	global_load_dwordx4 v[38:41], v[58:59], off sc0 nt
	global_load_dwordx4 v[50:53], v[60:61], off sc0 nt
	global_load_dwordx4 v[62:65], v[70:71], off sc0 nt
	s_nop 0
	global_load_dwordx4 v[58:61], v[72:73], off sc0 nt
	s_nop 0
	global_load_dwordx4 v[70:73], v[86:87], off sc0 nt
	global_load_dwordx4 v[82:85], v[88:89], off sc0 nt
	v_add_co_u32_e32 v86, vcc, s1, v2
	s_mov_b32 s1, 0x182c000
	s_nop 0
	v_addc_co_u32_e32 v87, vcc, 0, v3, vcc
	v_add_co_u32_e32 v88, vcc, s1, v2
	s_mov_b32 s1, 0x1830000
	s_nop 0
	v_addc_co_u32_e32 v89, vcc, 0, v3, vcc
	v_add_co_u32_e32 v98, vcc, s1, v2
	s_mov_b32 s1, 0x1834000
	s_nop 0
	v_addc_co_u32_e32 v99, vcc, 0, v3, vcc
	v_add_co_u32_e32 v106, vcc, s1, v2
	s_mov_b32 s1, 0x1838000
	s_nop 0
	v_addc_co_u32_e32 v107, vcc, 0, v3, vcc
	v_add_co_u32_e32 v114, vcc, s1, v2
	s_mov_b32 s1, 0x183c000
	s_nop 0
	v_addc_co_u32_e32 v115, vcc, 0, v3, vcc
	v_add_co_u32_e32 v116, vcc, s1, v2
	global_load_dwordx4 v[90:93], v[86:87], off sc0 nt
	s_nop 0
	global_load_dwordx4 v[86:89], v[88:89], off sc0 nt
	v_addc_co_u32_e32 v117, vcc, 0, v3, vcc
	global_load_dwordx4 v[98:101], v[98:99], off sc0 nt
	s_nop 0
	global_load_dwordx4 v[106:109], v[106:107], off sc0 nt
	s_nop 0
	global_load_dwordx4 v[122:125], v[114:115], off sc0 nt
	s_nop 0
	global_load_dwordx4 v[114:117], v[116:117], off sc0 nt
	ds_read_b128 v[130:133], v154
	ds_read_b128 v[138:141], v156
	ds_read_b128 v[142:145], v158
	ds_read_b128 v[146:149], v162
	s_waitcnt lgkmcnt(3)
	global_store_dwordx4 v[150:151], v[130:133], off offset:1024 nt
	s_waitcnt lgkmcnt(2)
	global_store_dwordx4 v[152:153], v[138:141], off offset:1024 nt
	s_waitcnt lgkmcnt(1)
	global_store_dwordx4 v[160:161], v[142:145], off offset:1024 nt
	s_waitcnt lgkmcnt(0)
	global_store_dwordx4 v[164:165], v[146:149], off offset:1024 nt
	s_waitcnt vmcnt(39)
	v_mul_f32_e32 v4, 0x43800000, v6
	s_waitcnt vmcnt(38)
	v_mul_f32_e32 v6, 0x43800000, v14
	v_med3_f32 v4, v4, s0, v1
	v_med3_f32 v6, v6, s0, v1
	v_mov_b32_e32 v130, v5
	v_cvt_pk_fp8_f32 v130, v4, v6
	s_waitcnt vmcnt(37)
	v_mul_f32_e32 v14, 0x43800000, v30
	s_waitcnt vmcnt(36)
	v_mul_f32_e32 v4, 0x43800000, v22
	v_med3_f32 v6, v14, s0, v1
	v_med3_f32 v4, v4, s0, v1
	v_cvt_pk_fp8_f32 v130, v6, v4 op_sel:[0,0,1]
	s_waitcnt vmcnt(35)
	v_mul_f32_e32 v4, 0x43800000, v42
	s_waitcnt vmcnt(34)
	v_mul_f32_e32 v6, 0x43800000, v46
	v_med3_f32 v4, v4, s0, v1
	v_med3_f32 v6, v6, s0, v1
	v_mov_b32_e32 v131, v5
	v_cvt_pk_fp8_f32 v131, v4, v6
	s_waitcnt vmcnt(33)
	v_mul_f32_e32 v14, 0x43800000, v66
	s_waitcnt vmcnt(32)
	v_mul_f32_e32 v4, 0x43800000, v54
	v_med3_f32 v6, v14, s0, v1
	v_med3_f32 v4, v4, s0, v1
	v_cvt_pk_fp8_f32 v131, v6, v4 op_sel:[0,0,1]
	s_waitcnt vmcnt(31)
	v_mul_f32_e32 v4, 0x43800000, v74
	s_waitcnt vmcnt(30)
	v_mul_f32_e32 v6, 0x43800000, v78
	v_med3_f32 v4, v4, s0, v1
	v_med3_f32 v6, v6, s0, v1
	v_mov_b32_e32 v132, v5
	v_cvt_pk_fp8_f32 v132, v4, v6
	s_waitcnt vmcnt(29)
	v_mul_f32_e32 v14, 0x43800000, v102
	s_waitcnt vmcnt(28)
	v_mul_f32_e32 v4, 0x43800000, v94
	v_med3_f32 v6, v14, s0, v1
	v_med3_f32 v4, v4, s0, v1
	v_cvt_pk_fp8_f32 v132, v6, v4 op_sel:[0,0,1]
	s_waitcnt vmcnt(27)
	v_mul_f32_e32 v4, 0x43800000, v110
	s_waitcnt vmcnt(26)
	v_mul_f32_e32 v6, 0x43800000, v118
	v_med3_f32 v4, v4, s0, v1
	v_med3_f32 v6, v6, s0, v1
	v_mov_b32_e32 v133, v5
	v_cvt_pk_fp8_f32 v133, v4, v6
	s_waitcnt vmcnt(25)
	v_mul_f32_e32 v14, 0x43800000, v134
	s_waitcnt vmcnt(24)
	v_mul_f32_e32 v4, 0x43800000, v126
	v_med3_f32 v6, v14, s0, v1
	v_med3_f32 v4, v4, s0, v1
	v_cvt_pk_fp8_f32 v133, v6, v4 op_sel:[0,0,1]
	v_mul_f32_e32 v4, 0x43800000, v7
	v_mul_f32_e32 v6, 0x43800000, v15
	v_med3_f32 v4, v4, s0, v1
	v_med3_f32 v6, v6, s0, v1
	v_mov_b32_e32 v138, v5
	v_cvt_pk_fp8_f32 v138, v4, v6
	v_mul_f32_e32 v7, 0x43800000, v31
	v_mul_f32_e32 v4, 0x43800000, v23
	v_med3_f32 v6, v7, s0, v1
	v_med3_f32 v4, v4, s0, v1
	v_cvt_pk_fp8_f32 v138, v6, v4 op_sel:[0,0,1]
	v_mul_f32_e32 v4, 0x43800000, v43
	v_mul_f32_e32 v6, 0x43800000, v47
	v_med3_f32 v4, v4, s0, v1
	v_med3_f32 v6, v6, s0, v1
	v_mov_b32_e32 v139, v5
	v_cvt_pk_fp8_f32 v139, v4, v6
	v_mul_f32_e32 v7, 0x43800000, v67
	v_mul_f32_e32 v4, 0x43800000, v55
	v_med3_f32 v6, v7, s0, v1
	v_med3_f32 v4, v4, s0, v1
	v_cvt_pk_fp8_f32 v139, v6, v4 op_sel:[0,0,1]
	v_mul_f32_e32 v4, 0x43800000, v75
	v_mul_f32_e32 v6, 0x43800000, v79
	v_med3_f32 v4, v4, s0, v1
	v_med3_f32 v6, v6, s0, v1
	v_mov_b32_e32 v140, v5
	v_cvt_pk_fp8_f32 v140, v4, v6
	v_mul_f32_e32 v7, 0x43800000, v103
	v_mul_f32_e32 v4, 0x43800000, v95
	v_med3_f32 v6, v7, s0, v1
	v_med3_f32 v4, v4, s0, v1
	v_cvt_pk_fp8_f32 v140, v6, v4 op_sel:[0,0,1]
	v_mul_f32_e32 v4, 0x43800000, v111
	v_mul_f32_e32 v6, 0x43800000, v119
	v_med3_f32 v4, v4, s0, v1
	v_med3_f32 v6, v6, s0, v1
	v_mov_b32_e32 v141, v5
	v_cvt_pk_fp8_f32 v141, v4, v6
	v_mul_f32_e32 v7, 0x43800000, v135
	v_mul_f32_e32 v4, 0x43800000, v127
	v_med3_f32 v6, v7, s0, v1
	v_med3_f32 v4, v4, s0, v1
	v_cvt_pk_fp8_f32 v141, v6, v4 op_sel:[0,0,1]
	v_mul_f32_e32 v4, 0x43800000, v8
	v_mul_f32_e32 v6, 0x43800000, v16
	v_med3_f32 v4, v4, s0, v1
	v_med3_f32 v6, v6, s0, v1
	v_mov_b32_e32 v142, v5
	v_cvt_pk_fp8_f32 v142, v4, v6
	v_mul_f32_e32 v7, 0x43800000, v32
	v_mul_f32_e32 v4, 0x43800000, v24
	v_med3_f32 v6, v7, s0, v1
	v_med3_f32 v4, v4, s0, v1
	v_cvt_pk_fp8_f32 v142, v6, v4 op_sel:[0,0,1]
	v_mul_f32_e32 v4, 0x43800000, v44
	v_mul_f32_e32 v6, 0x43800000, v48
	v_med3_f32 v4, v4, s0, v1
	v_med3_f32 v6, v6, s0, v1
	v_mov_b32_e32 v143, v5
	v_cvt_pk_fp8_f32 v143, v4, v6
	v_mul_f32_e32 v7, 0x43800000, v68
	v_mul_f32_e32 v4, 0x43800000, v56
	v_med3_f32 v6, v7, s0, v1
	v_med3_f32 v4, v4, s0, v1
	v_cvt_pk_fp8_f32 v143, v6, v4 op_sel:[0,0,1]
	v_mul_f32_e32 v4, 0x43800000, v76
	v_mul_f32_e32 v6, 0x43800000, v80
	v_med3_f32 v4, v4, s0, v1
	v_med3_f32 v6, v6, s0, v1
	v_mov_b32_e32 v144, v5
	v_cvt_pk_fp8_f32 v144, v4, v6
	v_mul_f32_e32 v7, 0x43800000, v104
	v_mul_f32_e32 v4, 0x43800000, v96
	v_med3_f32 v6, v7, s0, v1
	v_med3_f32 v4, v4, s0, v1
	v_cvt_pk_fp8_f32 v144, v6, v4 op_sel:[0,0,1]
	v_mul_f32_e32 v4, 0x43800000, v112
	v_mul_f32_e32 v6, 0x43800000, v120
	v_med3_f32 v4, v4, s0, v1
	v_med3_f32 v6, v6, s0, v1
	v_mov_b32_e32 v145, v5
	v_cvt_pk_fp8_f32 v145, v4, v6
	v_mul_f32_e32 v7, 0x43800000, v136
	v_mul_f32_e32 v4, 0x43800000, v128
	v_med3_f32 v6, v7, s0, v1
	v_med3_f32 v4, v4, s0, v1
	v_cvt_pk_fp8_f32 v145, v6, v4 op_sel:[0,0,1]
	v_mul_f32_e32 v4, 0x43800000, v9
	v_mul_f32_e32 v6, 0x43800000, v17
	v_med3_f32 v4, v4, s0, v1
	v_med3_f32 v8, v6, s0, v1
	v_mov_b32_e32 v6, v5
	v_cvt_pk_fp8_f32 v6, v4, v8
	v_mul_f32_e32 v7, 0x43800000, v33
	v_mul_f32_e32 v4, 0x43800000, v25
	v_med3_f32 v7, v7, s0, v1
	v_med3_f32 v4, v4, s0, v1
	v_cvt_pk_fp8_f32 v6, v7, v4 op_sel:[0,0,1]
	v_mul_f32_e32 v4, 0x43800000, v45
	v_mul_f32_e32 v7, 0x43800000, v49
	v_med3_f32 v4, v4, s0, v1
	v_med3_f32 v9, v7, s0, v1
	v_mov_b32_e32 v7, v5
	v_cvt_pk_fp8_f32 v7, v4, v9
	v_mul_f32_e32 v8, 0x43800000, v69
	v_mul_f32_e32 v4, 0x43800000, v57
	v_med3_f32 v8, v8, s0, v1
	v_med3_f32 v4, v4, s0, v1
	v_cvt_pk_fp8_f32 v7, v8, v4 op_sel:[0,0,1]
	v_mul_f32_e32 v4, 0x43800000, v77
	v_mul_f32_e32 v8, 0x43800000, v81
	v_med3_f32 v4, v4, s0, v1
	v_med3_f32 v14, v8, s0, v1
	v_mov_b32_e32 v8, v5
	v_cvt_pk_fp8_f32 v8, v4, v14
	v_mul_f32_e32 v9, 0x43800000, v105
	v_mul_f32_e32 v4, 0x43800000, v97
	v_med3_f32 v9, v9, s0, v1
	v_med3_f32 v4, v4, s0, v1
	v_cvt_pk_fp8_f32 v8, v9, v4 op_sel:[0,0,1]
	v_mul_f32_e32 v4, 0x43800000, v113
	v_mul_f32_e32 v9, 0x43800000, v121
	v_med3_f32 v4, v4, s0, v1
	v_med3_f32 v15, v9, s0, v1
	v_mov_b32_e32 v9, v5
	v_cvt_pk_fp8_f32 v9, v4, v15
	v_mul_f32_e32 v14, 0x43800000, v137
	v_mul_f32_e32 v4, 0x43800000, v129
	v_med3_f32 v14, v14, s0, v1
	v_med3_f32 v4, v4, s0, v1
	v_cvt_pk_fp8_f32 v9, v14, v4 op_sel:[0,0,1]
	ds_write_b128 v166, v[130:133] offset:34816
	ds_write_b128 v166, v[138:141] offset:35088
	ds_write_b128 v166, v[142:145] offset:35360
	ds_write_b128 v166, v[6:9] offset:35632
	s_waitcnt lgkmcnt(0)
	s_barrier
	s_mov_b32 s1, 0x1c00000
	v_add_co_u32_e32 v6, vcc, s1, v2
	s_mov_b32 s1, 0x1c04000
	s_nop 0
	v_addc_co_u32_e32 v7, vcc, 0, v3, vcc
	v_add_co_u32_e32 v14, vcc, s1, v2
	s_mov_b32 s1, 0x1c08000
	s_nop 0
	v_addc_co_u32_e32 v15, vcc, 0, v3, vcc
	v_add_co_u32_e32 v42, vcc, s1, v2
	s_mov_b32 s1, 0x1c0c000
	s_nop 0
	v_addc_co_u32_e32 v43, vcc, 0, v3, vcc
	v_add_co_u32_e32 v44, vcc, s1, v2
	s_mov_b32 s1, 0x1c10000
	s_nop 0
	v_addc_co_u32_e32 v45, vcc, 0, v3, vcc
	v_add_co_u32_e32 v54, vcc, s1, v2
	s_mov_b32 s1, 0x1c14000
	s_nop 0
	v_addc_co_u32_e32 v55, vcc, 0, v3, vcc
	v_add_co_u32_e32 v56, vcc, s1, v2
	s_mov_b32 s1, 0x1c18000
	s_nop 0
	v_addc_co_u32_e32 v57, vcc, 0, v3, vcc
	v_add_co_u32_e32 v74, vcc, s1, v2
	s_mov_b32 s1, 0x1c1c000
	s_nop 0
	v_addc_co_u32_e32 v75, vcc, 0, v3, vcc
	v_add_co_u32_e32 v76, vcc, s1, v2
	s_mov_b32 s1, 0x1c20000
	s_nop 0
	v_addc_co_u32_e32 v77, vcc, 0, v3, vcc
	v_add_co_u32_e32 v94, vcc, s1, v2
	s_mov_b32 s1, 0x1c24000
	s_nop 0
	v_addc_co_u32_e32 v95, vcc, 0, v3, vcc
	v_add_co_u32_e32 v96, vcc, s1, v2
	s_mov_b32 s1, 0x1c28000
	s_nop 0
	v_addc_co_u32_e32 v97, vcc, 0, v3, vcc
	global_load_dwordx4 v[6:9], v[6:7], off sc0 nt
	s_nop 0
	global_load_dwordx4 v[14:17], v[14:15], off sc0 nt
	s_nop 0
	global_load_dwordx4 v[30:33], v[42:43], off sc0 nt
	global_load_dwordx4 v[22:25], v[44:45], off sc0 nt
	s_nop 0
	global_load_dwordx4 v[42:45], v[54:55], off sc0 nt
	global_load_dwordx4 v[46:49], v[56:57], off sc0 nt
	global_load_dwordx4 v[66:69], v[74:75], off sc0 nt
	s_nop 0
	global_load_dwordx4 v[54:57], v[76:77], off sc0 nt
	s_nop 0
	global_load_dwordx4 v[74:77], v[94:95], off sc0 nt
	global_load_dwordx4 v[78:81], v[96:97], off sc0 nt
	v_add_co_u32_e32 v94, vcc, s1, v2
	s_mov_b32 s1, 0x1c2c000
	s_nop 0
	v_addc_co_u32_e32 v95, vcc, 0, v3, vcc
	v_add_co_u32_e32 v96, vcc, s1, v2
	s_mov_b32 s1, 0x1c30000
	s_nop 0
	v_addc_co_u32_e32 v97, vcc, 0, v3, vcc
	v_add_co_u32_e32 v110, vcc, s1, v2
	s_mov_b32 s1, 0x1c34000
	s_nop 0
	v_addc_co_u32_e32 v111, vcc, 0, v3, vcc
	v_add_co_u32_e32 v118, vcc, s1, v2
	s_mov_b32 s1, 0x1c38000
	s_nop 0
	v_addc_co_u32_e32 v119, vcc, 0, v3, vcc
	v_add_co_u32_e32 v126, vcc, s1, v2
	s_mov_b32 s1, 0x1c3c000
	s_nop 0
	v_addc_co_u32_e32 v127, vcc, 0, v3, vcc
	v_add_co_u32_e32 v2, vcc, s1, v2
	global_load_dwordx4 v[102:105], v[94:95], off sc0 nt
	s_nop 0
	global_load_dwordx4 v[94:97], v[96:97], off sc0 nt
	s_nop 0
	global_load_dwordx4 v[110:113], v[110:111], off sc0 nt
	s_nop 0
	global_load_dwordx4 v[118:121], v[118:119], off sc0 nt
	v_addc_co_u32_e32 v3, vcc, 0, v3, vcc
	global_load_dwordx4 v[130:133], v[126:127], off sc0 nt
	s_nop 0
	global_load_dwordx4 v[126:129], v[2:3], off sc0 nt
	ds_read_b128 v[134:137], v154 offset:34816
	ds_read_b128 v[138:141], v156 offset:34816
	ds_read_b128 v[142:145], v158 offset:34816
	ds_read_b128 v[146:149], v162 offset:34816
	s_waitcnt lgkmcnt(3)
	global_store_dwordx4 v[150:151], v[134:137], off offset:1280 nt
	s_waitcnt lgkmcnt(2)
	global_store_dwordx4 v[152:153], v[138:141], off offset:1280 nt
	s_waitcnt lgkmcnt(1)
	global_store_dwordx4 v[160:161], v[142:145], off offset:1280 nt
	s_waitcnt lgkmcnt(0)
	global_store_dwordx4 v[164:165], v[146:149], off offset:1280 nt
	s_waitcnt vmcnt(39)
	v_mul_f32_e32 v2, 0x43800000, v10
	s_waitcnt vmcnt(38)
	v_mul_f32_e32 v3, 0x43800000, v18
	v_med3_f32 v2, v2, s0, v1
	v_med3_f32 v3, v3, s0, v1
	v_mov_b32_e32 v134, v5
	v_cvt_pk_fp8_f32 v134, v2, v3
	s_waitcnt vmcnt(37)
	v_mul_f32_e32 v4, 0x43800000, v34
	s_waitcnt vmcnt(36)
	v_mul_f32_e32 v2, 0x43800000, v26
	v_med3_f32 v3, v4, s0, v1
	v_med3_f32 v2, v2, s0, v1
	v_cvt_pk_fp8_f32 v134, v3, v2 op_sel:[0,0,1]
	s_waitcnt vmcnt(35)
	v_mul_f32_e32 v2, 0x43800000, v38
	s_waitcnt vmcnt(34)
	v_mul_f32_e32 v3, 0x43800000, v50
	v_med3_f32 v2, v2, s0, v1
	v_med3_f32 v3, v3, s0, v1
	v_mov_b32_e32 v135, v5
	v_cvt_pk_fp8_f32 v135, v2, v3
	s_waitcnt vmcnt(33)
	v_mul_f32_e32 v4, 0x43800000, v62
	s_waitcnt vmcnt(32)
	v_mul_f32_e32 v2, 0x43800000, v58
	v_med3_f32 v3, v4, s0, v1
	v_med3_f32 v2, v2, s0, v1
	v_cvt_pk_fp8_f32 v135, v3, v2 op_sel:[0,0,1]
	s_waitcnt vmcnt(31)
	v_mul_f32_e32 v2, 0x43800000, v70
	s_waitcnt vmcnt(30)
	v_mul_f32_e32 v3, 0x43800000, v82
	v_med3_f32 v2, v2, s0, v1
	v_med3_f32 v3, v3, s0, v1
	v_mov_b32_e32 v136, v5
	v_cvt_pk_fp8_f32 v136, v2, v3
	s_waitcnt vmcnt(29)
	v_mul_f32_e32 v4, 0x43800000, v90
	s_waitcnt vmcnt(28)
	v_mul_f32_e32 v2, 0x43800000, v86
	v_med3_f32 v3, v4, s0, v1
	v_med3_f32 v2, v2, s0, v1
	v_cvt_pk_fp8_f32 v136, v3, v2 op_sel:[0,0,1]
	s_waitcnt vmcnt(27)
	v_mul_f32_e32 v2, 0x43800000, v98
	s_waitcnt vmcnt(26)
	v_mul_f32_e32 v3, 0x43800000, v106
	v_med3_f32 v2, v2, s0, v1
	v_med3_f32 v3, v3, s0, v1
	v_mov_b32_e32 v137, v5
	v_cvt_pk_fp8_f32 v137, v2, v3
	s_waitcnt vmcnt(25)
	v_mul_f32_e32 v4, 0x43800000, v122
	s_waitcnt vmcnt(24)
	v_mul_f32_e32 v2, 0x43800000, v114
	v_med3_f32 v3, v4, s0, v1
	v_med3_f32 v2, v2, s0, v1
	v_cvt_pk_fp8_f32 v137, v3, v2 op_sel:[0,0,1]
	v_mul_f32_e32 v2, 0x43800000, v11
	v_mul_f32_e32 v3, 0x43800000, v19
	v_med3_f32 v2, v2, s0, v1
	v_med3_f32 v3, v3, s0, v1
	v_mov_b32_e32 v138, v5
	v_cvt_pk_fp8_f32 v138, v2, v3
	v_mul_f32_e32 v4, 0x43800000, v35
	v_mul_f32_e32 v2, 0x43800000, v27
	v_med3_f32 v3, v4, s0, v1
	v_med3_f32 v2, v2, s0, v1
	v_cvt_pk_fp8_f32 v138, v3, v2 op_sel:[0,0,1]
	v_mul_f32_e32 v2, 0x43800000, v39
	v_mul_f32_e32 v3, 0x43800000, v51
	v_med3_f32 v2, v2, s0, v1
	v_med3_f32 v3, v3, s0, v1
	v_mov_b32_e32 v139, v5
	v_cvt_pk_fp8_f32 v139, v2, v3
	v_mul_f32_e32 v4, 0x43800000, v63
	v_mul_f32_e32 v2, 0x43800000, v59
	v_med3_f32 v3, v4, s0, v1
	v_med3_f32 v2, v2, s0, v1
	v_cvt_pk_fp8_f32 v139, v3, v2 op_sel:[0,0,1]
	v_mul_f32_e32 v2, 0x43800000, v71
	v_mul_f32_e32 v3, 0x43800000, v83
	v_med3_f32 v2, v2, s0, v1
	v_med3_f32 v3, v3, s0, v1
	v_mov_b32_e32 v140, v5
	v_cvt_pk_fp8_f32 v140, v2, v3
	v_mul_f32_e32 v4, 0x43800000, v91
	v_mul_f32_e32 v2, 0x43800000, v87
	v_med3_f32 v3, v4, s0, v1
	v_med3_f32 v2, v2, s0, v1
	v_cvt_pk_fp8_f32 v140, v3, v2 op_sel:[0,0,1]
	v_mul_f32_e32 v2, 0x43800000, v99
	v_mul_f32_e32 v3, 0x43800000, v107
	v_med3_f32 v2, v2, s0, v1
	v_med3_f32 v3, v3, s0, v1
	v_mov_b32_e32 v141, v5
	v_cvt_pk_fp8_f32 v141, v2, v3
	v_mul_f32_e32 v4, 0x43800000, v123
	v_mul_f32_e32 v2, 0x43800000, v115
	v_med3_f32 v3, v4, s0, v1
	v_med3_f32 v2, v2, s0, v1
	v_cvt_pk_fp8_f32 v141, v3, v2 op_sel:[0,0,1]
	v_mul_f32_e32 v2, 0x43800000, v12
	v_mul_f32_e32 v3, 0x43800000, v20
	v_med3_f32 v2, v2, s0, v1
	v_med3_f32 v3, v3, s0, v1
	v_mov_b32_e32 v142, v5
	v_cvt_pk_fp8_f32 v142, v2, v3
	v_mul_f32_e32 v4, 0x43800000, v36
	v_mul_f32_e32 v2, 0x43800000, v28
	v_med3_f32 v3, v4, s0, v1
	v_med3_f32 v2, v2, s0, v1
	v_cvt_pk_fp8_f32 v142, v3, v2 op_sel:[0,0,1]
	v_mul_f32_e32 v2, 0x43800000, v40
	v_mul_f32_e32 v3, 0x43800000, v52
	v_med3_f32 v2, v2, s0, v1
	v_med3_f32 v3, v3, s0, v1
	v_mov_b32_e32 v143, v5
	v_cvt_pk_fp8_f32 v143, v2, v3
	v_mul_f32_e32 v4, 0x43800000, v64
	v_mul_f32_e32 v2, 0x43800000, v60
	v_med3_f32 v3, v4, s0, v1
	v_med3_f32 v2, v2, s0, v1
	v_cvt_pk_fp8_f32 v143, v3, v2 op_sel:[0,0,1]
	v_mul_f32_e32 v2, 0x43800000, v72
	v_mul_f32_e32 v3, 0x43800000, v84
	v_med3_f32 v2, v2, s0, v1
	v_med3_f32 v3, v3, s0, v1
	v_mov_b32_e32 v144, v5
	v_cvt_pk_fp8_f32 v144, v2, v3
	v_mul_f32_e32 v4, 0x43800000, v92
	v_mul_f32_e32 v2, 0x43800000, v88
	v_med3_f32 v3, v4, s0, v1
	v_med3_f32 v2, v2, s0, v1
	v_cvt_pk_fp8_f32 v144, v3, v2 op_sel:[0,0,1]
	v_mul_f32_e32 v2, 0x43800000, v100
	v_mul_f32_e32 v3, 0x43800000, v108
	v_med3_f32 v2, v2, s0, v1
	v_med3_f32 v3, v3, s0, v1
	v_mov_b32_e32 v145, v5
	v_cvt_pk_fp8_f32 v145, v2, v3
	v_mul_f32_e32 v4, 0x43800000, v124
	v_mul_f32_e32 v2, 0x43800000, v116
	v_med3_f32 v3, v4, s0, v1
	v_med3_f32 v2, v2, s0, v1
	v_cvt_pk_fp8_f32 v145, v3, v2 op_sel:[0,0,1]
	v_mul_f32_e32 v2, 0x43800000, v13
	v_mul_f32_e32 v3, 0x43800000, v21
	v_med3_f32 v2, v2, s0, v1
	v_med3_f32 v3, v3, s0, v1
	v_mov_b32_e32 v10, v5
	v_cvt_pk_fp8_f32 v10, v2, v3
	v_mul_f32_e32 v4, 0x43800000, v37
	v_mul_f32_e32 v2, 0x43800000, v29
	v_med3_f32 v3, v4, s0, v1
	v_med3_f32 v2, v2, s0, v1
	v_cvt_pk_fp8_f32 v10, v3, v2 op_sel:[0,0,1]
	v_mul_f32_e32 v2, 0x43800000, v41
	v_mul_f32_e32 v3, 0x43800000, v53
	v_med3_f32 v2, v2, s0, v1
	v_med3_f32 v3, v3, s0, v1
	v_mov_b32_e32 v11, v5
	v_cvt_pk_fp8_f32 v11, v2, v3
	v_mul_f32_e32 v4, 0x43800000, v65
	v_mul_f32_e32 v2, 0x43800000, v61
	v_med3_f32 v3, v4, s0, v1
	v_med3_f32 v2, v2, s0, v1
	v_cvt_pk_fp8_f32 v11, v3, v2 op_sel:[0,0,1]
	v_mul_f32_e32 v2, 0x43800000, v73
	v_mul_f32_e32 v3, 0x43800000, v85
	v_med3_f32 v2, v2, s0, v1
	v_med3_f32 v3, v3, s0, v1
	v_mov_b32_e32 v12, v5
	v_cvt_pk_fp8_f32 v12, v2, v3
	v_mul_f32_e32 v4, 0x43800000, v93
	v_mul_f32_e32 v2, 0x43800000, v89
	v_med3_f32 v3, v4, s0, v1
	v_med3_f32 v2, v2, s0, v1
	v_cvt_pk_fp8_f32 v12, v3, v2 op_sel:[0,0,1]
	v_mul_f32_e32 v2, 0x43800000, v101
	v_mul_f32_e32 v3, 0x43800000, v109
	v_med3_f32 v2, v2, s0, v1
	v_med3_f32 v3, v3, s0, v1
	v_mov_b32_e32 v13, v5
	v_cvt_pk_fp8_f32 v13, v2, v3
	v_mul_f32_e32 v4, 0x43800000, v125
	v_mul_f32_e32 v2, 0x43800000, v117
	v_med3_f32 v3, v4, s0, v1
	v_med3_f32 v2, v2, s0, v1
	v_cvt_pk_fp8_f32 v13, v3, v2 op_sel:[0,0,1]
	ds_write_b128 v166, v[134:137]
	ds_write_b128 v166, v[138:141] offset:272
	ds_write_b128 v166, v[142:145] offset:544
	ds_write_b128 v166, v[10:13] offset:816
	s_waitcnt lgkmcnt(0)
	s_barrier
	ds_read_b128 v[10:13], v154
	ds_read_b128 v[18:21], v156
	ds_read_b128 v[26:29], v158
	ds_read_b128 v[34:37], v162
	s_waitcnt lgkmcnt(3)
	global_store_dwordx4 v[150:151], v[10:13], off offset:1536 nt
	s_waitcnt lgkmcnt(2)
	global_store_dwordx4 v[152:153], v[18:21], off offset:1536 nt
	s_waitcnt lgkmcnt(1)
	global_store_dwordx4 v[160:161], v[26:29], off offset:1536 nt
	s_waitcnt lgkmcnt(0)
	global_store_dwordx4 v[164:165], v[34:37], off offset:1536 nt
	s_waitcnt vmcnt(23)
	v_mul_f32_e32 v2, 0x43800000, v6
	s_waitcnt vmcnt(22)
	v_mul_f32_e32 v3, 0x43800000, v14
	v_med3_f32 v2, v2, s0, v1
	v_med3_f32 v3, v3, s0, v1
	v_mov_b32_e32 v10, v5
	v_cvt_pk_fp8_f32 v10, v2, v3
	s_waitcnt vmcnt(21)
	v_mul_f32_e32 v4, 0x43800000, v30
	s_waitcnt vmcnt(20)
	v_mul_f32_e32 v2, 0x43800000, v22
	v_med3_f32 v3, v4, s0, v1
	v_med3_f32 v2, v2, s0, v1
	v_cvt_pk_fp8_f32 v10, v3, v2 op_sel:[0,0,1]
	s_waitcnt vmcnt(19)
	v_mul_f32_e32 v2, 0x43800000, v42
	s_waitcnt vmcnt(18)
	v_mul_f32_e32 v3, 0x43800000, v46
	v_med3_f32 v2, v2, s0, v1
	v_med3_f32 v3, v3, s0, v1
	v_mov_b32_e32 v11, v5
	v_cvt_pk_fp8_f32 v11, v2, v3
	s_waitcnt vmcnt(17)
	v_mul_f32_e32 v4, 0x43800000, v66
	s_waitcnt vmcnt(16)
	v_mul_f32_e32 v2, 0x43800000, v54
	v_med3_f32 v3, v4, s0, v1
	v_med3_f32 v2, v2, s0, v1
	v_cvt_pk_fp8_f32 v11, v3, v2 op_sel:[0,0,1]
	s_waitcnt vmcnt(15)
	v_mul_f32_e32 v2, 0x43800000, v74
	s_waitcnt vmcnt(14)
	v_mul_f32_e32 v3, 0x43800000, v78
	v_med3_f32 v2, v2, s0, v1
	v_med3_f32 v3, v3, s0, v1
	v_mov_b32_e32 v12, v5
	v_cvt_pk_fp8_f32 v12, v2, v3
	s_waitcnt vmcnt(13)
	v_mul_f32_e32 v4, 0x43800000, v102
	s_waitcnt vmcnt(12)
	v_mul_f32_e32 v2, 0x43800000, v94
	v_med3_f32 v3, v4, s0, v1
	v_med3_f32 v2, v2, s0, v1
	v_cvt_pk_fp8_f32 v12, v3, v2 op_sel:[0,0,1]
	s_waitcnt vmcnt(11)
	v_mul_f32_e32 v2, 0x43800000, v110
	s_waitcnt vmcnt(10)
	v_mul_f32_e32 v3, 0x43800000, v118
	v_med3_f32 v2, v2, s0, v1
	v_med3_f32 v3, v3, s0, v1
	v_mov_b32_e32 v13, v5
	v_cvt_pk_fp8_f32 v13, v2, v3
	s_waitcnt vmcnt(9)
	v_mul_f32_e32 v4, 0x43800000, v130
	s_waitcnt vmcnt(8)
	v_mul_f32_e32 v2, 0x43800000, v126
	v_med3_f32 v3, v4, s0, v1
	v_med3_f32 v2, v2, s0, v1
	v_cvt_pk_fp8_f32 v13, v3, v2 op_sel:[0,0,1]
	v_mul_f32_e32 v2, 0x43800000, v7
	v_mul_f32_e32 v3, 0x43800000, v15
	v_med3_f32 v2, v2, s0, v1
	v_med3_f32 v3, v3, s0, v1
	v_mov_b32_e32 v18, v5
	v_cvt_pk_fp8_f32 v18, v2, v3
	v_mul_f32_e32 v4, 0x43800000, v31
	v_mul_f32_e32 v2, 0x43800000, v23
	v_med3_f32 v3, v4, s0, v1
	v_med3_f32 v2, v2, s0, v1
	v_cvt_pk_fp8_f32 v18, v3, v2 op_sel:[0,0,1]
	v_mul_f32_e32 v2, 0x43800000, v43
	v_mul_f32_e32 v3, 0x43800000, v47
	v_med3_f32 v2, v2, s0, v1
	v_med3_f32 v3, v3, s0, v1
	v_mov_b32_e32 v19, v5
	v_cvt_pk_fp8_f32 v19, v2, v3
	v_mul_f32_e32 v4, 0x43800000, v67
	v_mul_f32_e32 v2, 0x43800000, v55
	v_med3_f32 v3, v4, s0, v1
	v_med3_f32 v2, v2, s0, v1
	v_cvt_pk_fp8_f32 v19, v3, v2 op_sel:[0,0,1]
	v_mul_f32_e32 v2, 0x43800000, v75
	v_mul_f32_e32 v3, 0x43800000, v79
	v_med3_f32 v2, v2, s0, v1
	v_med3_f32 v3, v3, s0, v1
	v_mov_b32_e32 v20, v5
	v_cvt_pk_fp8_f32 v20, v2, v3
	v_mul_f32_e32 v4, 0x43800000, v103
	v_mul_f32_e32 v2, 0x43800000, v95
	v_med3_f32 v3, v4, s0, v1
	v_med3_f32 v2, v2, s0, v1
	v_cvt_pk_fp8_f32 v20, v3, v2 op_sel:[0,0,1]
	v_mul_f32_e32 v2, 0x43800000, v111
	v_mul_f32_e32 v3, 0x43800000, v119
	v_med3_f32 v2, v2, s0, v1
	v_med3_f32 v3, v3, s0, v1
	v_mov_b32_e32 v21, v5
	v_cvt_pk_fp8_f32 v21, v2, v3
	v_mul_f32_e32 v4, 0x43800000, v131
	v_mul_f32_e32 v2, 0x43800000, v127
	v_med3_f32 v3, v4, s0, v1
	v_med3_f32 v2, v2, s0, v1
	v_cvt_pk_fp8_f32 v21, v3, v2 op_sel:[0,0,1]
	v_mul_f32_e32 v2, 0x43800000, v8
	v_mul_f32_e32 v3, 0x43800000, v16
	v_med3_f32 v2, v2, s0, v1
	v_med3_f32 v3, v3, s0, v1
	v_mov_b32_e32 v26, v5
	v_cvt_pk_fp8_f32 v26, v2, v3
	v_mul_f32_e32 v4, 0x43800000, v32
	v_mul_f32_e32 v2, 0x43800000, v24
	v_med3_f32 v3, v4, s0, v1
	v_med3_f32 v2, v2, s0, v1
	v_cvt_pk_fp8_f32 v26, v3, v2 op_sel:[0,0,1]
	v_mul_f32_e32 v2, 0x43800000, v44
	v_mul_f32_e32 v3, 0x43800000, v48
	v_med3_f32 v2, v2, s0, v1
	v_med3_f32 v3, v3, s0, v1
	v_mov_b32_e32 v27, v5
	v_cvt_pk_fp8_f32 v27, v2, v3
	v_mul_f32_e32 v4, 0x43800000, v68
	v_mul_f32_e32 v2, 0x43800000, v56
	v_med3_f32 v3, v4, s0, v1
	v_med3_f32 v2, v2, s0, v1
	v_cvt_pk_fp8_f32 v27, v3, v2 op_sel:[0,0,1]
	v_mul_f32_e32 v2, 0x43800000, v76
	v_mul_f32_e32 v3, 0x43800000, v80
	v_med3_f32 v2, v2, s0, v1
	v_med3_f32 v3, v3, s0, v1
	v_mov_b32_e32 v28, v5
	v_cvt_pk_fp8_f32 v28, v2, v3
	v_mul_f32_e32 v4, 0x43800000, v104
	v_mul_f32_e32 v2, 0x43800000, v96
	v_med3_f32 v3, v4, s0, v1
	v_med3_f32 v2, v2, s0, v1
	v_cvt_pk_fp8_f32 v28, v3, v2 op_sel:[0,0,1]
	v_mul_f32_e32 v2, 0x43800000, v112
	v_mul_f32_e32 v3, 0x43800000, v120
	v_med3_f32 v2, v2, s0, v1
	v_med3_f32 v3, v3, s0, v1
	v_mov_b32_e32 v29, v5
	v_cvt_pk_fp8_f32 v29, v2, v3
	v_mul_f32_e32 v4, 0x43800000, v132
	v_mul_f32_e32 v2, 0x43800000, v128
	v_med3_f32 v3, v4, s0, v1
	v_med3_f32 v2, v2, s0, v1
	v_cvt_pk_fp8_f32 v29, v3, v2 op_sel:[0,0,1]
	v_mul_f32_e32 v2, 0x43800000, v9
	v_mul_f32_e32 v3, 0x43800000, v17
	v_med3_f32 v6, v2, s0, v1
	v_med3_f32 v3, v3, s0, v1
	v_mov_b32_e32 v2, v5
	v_cvt_pk_fp8_f32 v2, v6, v3
	v_mul_f32_e32 v4, 0x43800000, v33
	v_mul_f32_e32 v3, 0x43800000, v25
	v_med3_f32 v4, v4, s0, v1
	v_med3_f32 v3, v3, s0, v1
	v_cvt_pk_fp8_f32 v2, v4, v3 op_sel:[0,0,1]
	v_mul_f32_e32 v3, 0x43800000, v45
	v_mul_f32_e32 v4, 0x43800000, v49
	v_med3_f32 v7, v3, s0, v1
	v_med3_f32 v4, v4, s0, v1
	v_mov_b32_e32 v3, v5
	v_cvt_pk_fp8_f32 v3, v7, v4
	v_mul_f32_e32 v6, 0x43800000, v69
	v_mul_f32_e32 v4, 0x43800000, v57
	v_med3_f32 v6, v6, s0, v1
	v_med3_f32 v4, v4, s0, v1
	v_cvt_pk_fp8_f32 v3, v6, v4 op_sel:[0,0,1]
	v_mul_f32_e32 v4, 0x43800000, v77
	v_mul_f32_e32 v6, 0x43800000, v81
	v_med3_f32 v8, v4, s0, v1
	v_med3_f32 v6, v6, s0, v1
	v_mov_b32_e32 v4, v5
	v_cvt_pk_fp8_f32 v4, v8, v6
	v_mul_f32_e32 v7, 0x43800000, v105
	v_mul_f32_e32 v6, 0x43800000, v97
	v_med3_f32 v7, v7, s0, v1
	v_med3_f32 v6, v6, s0, v1
	v_cvt_pk_fp8_f32 v4, v7, v6 op_sel:[0,0,1]
	v_mul_f32_e32 v6, 0x43800000, v113
	v_mul_f32_e32 v7, 0x43800000, v121
	v_med3_f32 v6, v6, s0, v1
	v_med3_f32 v7, v7, s0, v1
	v_cvt_pk_fp8_f32 v5, v6, v7
	v_mul_f32_e32 v8, 0x43800000, v133
	v_mul_f32_e32 v6, 0x43800000, v129
	v_med3_f32 v7, v8, s0, v1
	v_med3_f32 v1, v6, s0, v1
	v_cvt_pk_fp8_f32 v5, v7, v1 op_sel:[0,0,1]
	ds_write_b128 v166, v[10:13] offset:34816
	ds_write_b128 v166, v[18:21] offset:35088
	ds_write_b128 v166, v[26:29] offset:35360
	ds_write_b128 v166, v[2:5] offset:35632
	s_waitcnt lgkmcnt(0)
	s_barrier
	ds_read_b128 v[2:5], v154 offset:34816
	ds_read_b128 v[6:9], v156 offset:34816
	ds_read_b128 v[10:13], v158 offset:34816
	ds_read_b128 v[14:17], v162 offset:34816
	s_waitcnt lgkmcnt(3)
	global_store_dwordx4 v[150:151], v[2:5], off offset:1792 nt
	s_waitcnt lgkmcnt(2)
	global_store_dwordx4 v[152:153], v[6:9], off offset:1792 nt
	s_waitcnt lgkmcnt(1)
	global_store_dwordx4 v[160:161], v[10:13], off offset:1792 nt
	s_waitcnt lgkmcnt(0)
	global_store_dwordx4 v[164:165], v[14:17], off offset:1792 nt
	s_barrier

.LBB0_1081:
	s_cmp_eq_u32 s0, 0
	s_cselect_b64 s[0:1], -1, 0
	s_or_b64 s[0:1], s[0:1], s[10:11]
	s_mov_b64 s[6:7], -1
	s_and_b64 vcc, exec, s[0:1]
	s_branch .LBB0_1087
	s_cmp_gt_i32 s74, -1
	s_cbranch_scc0 .LBB0_1084
	s_lshr_b32 s0, s74, 4
	s_mov_b32 s1, 0
	v_readlane_b32 s12, v254, 4
	s_lshl_b64 s[2:3], s[0:1], 24
	v_readlane_b32 s18, v254, 10
	v_readlane_b32 s19, v254, 11
	s_add_u32 s2, s18, s2
	s_addc_u32 s3, s19, s3
	s_lshl_b32 s5, s74, 7
	s_and_b32 s5, s5, 0x780
	s_lshl_b32 s6, s5, 2
	s_add_u32 s2, s2, s6
	s_addc_u32 s3, s3, 0
	s_lshl_b64 s[0:1], s[0:1], 22
	s_lshl_b32 s5, s5, 11
	s_add_u32 s0, s78, s0
	v_mov_b32_e32 v134, v0
	s_addc_u32 s1, s79, s1
	s_add_u32 s6, s0, s5
	v_readfirstlane_b32 s4, v134
	s_addc_u32 s7, s1, 0
	s_ashr_i32 s0, s4, 1
	v_lshrrev_b32_e32 v1, 1, v134
	s_andn2_b32 s0, s0, 31
	v_and_b32_e32 v135, 16, v1
	v_or_b32_e32 v2, s0, v135
	v_ashrrev_i32_e32 v3, 31, v2
	v_lshlrev_b32_e32 v1, 2, v134
	v_lshlrev_b64 v[2:3], 13, v[2:3]
	v_and_b32_e32 v140, 0x7c, v1
	v_lshl_add_u64 v[2:3], s[2:3], 0, v[2:3]
	v_lshlrev_b32_e32 v4, 2, v140
	v_mov_b32_e32 v5, 0
	v_lshl_add_u64 v[2:3], v[2:3], 0, v[4:5]
	s_movk_i32 s1, 0x2000
	v_add_co_u32_e32 v6, vcc, s1, v2
	s_movk_i32 s1, 0x4000
	s_nop 0
	v_addc_co_u32_e32 v7, vcc, 0, v3, vcc
	global_load_dwordx4 v[34:37], v[2:3], off sc0 nt
	global_load_dwordx4 v[38:41], v[6:7], off sc0 nt
	v_add_co_u32_e32 v6, vcc, s1, v2
	s_movk_i32 s1, 0x6000
	s_nop 0
	v_addc_co_u32_e32 v7, vcc, 0, v3, vcc
	v_add_co_u32_e32 v8, vcc, s1, v2
	s_mov_b32 s1, 0x8000
	s_nop 0
	v_addc_co_u32_e32 v9, vcc, 0, v3, vcc
	global_load_dwordx4 v[58:61], v[6:7], off sc0 nt
	global_load_dwordx4 v[50:53], v[8:9], off sc0 nt
	v_add_co_u32_e32 v6, vcc, s1, v2
	s_mov_b32 s1, 0xa000
	s_nop 0
	v_addc_co_u32_e32 v7, vcc, 0, v3, vcc
	v_add_co_u32_e32 v8, vcc, s1, v2
	s_mov_b32 s1, 0xc000
	s_nop 0
	v_addc_co_u32_e32 v9, vcc, 0, v3, vcc
	global_load_dwordx4 v[66:69], v[6:7], off sc0 nt
	global_load_dwordx4 v[70:73], v[8:9], off sc0 nt
	v_add_co_u32_e32 v6, vcc, s1, v2
	s_mov_b32 s1, 0xe000
	s_nop 0
	v_addc_co_u32_e32 v7, vcc, 0, v3, vcc
	v_add_co_u32_e32 v8, vcc, s1, v2
	s_mov_b32 s1, 0x10000
	s_nop 0
	v_addc_co_u32_e32 v9, vcc, 0, v3, vcc
	global_load_dwordx4 v[94:97], v[6:7], off sc0 nt
	global_load_dwordx4 v[82:85], v[8:9], off sc0 nt
	v_add_co_u32_e32 v6, vcc, s1, v2
	s_mov_b32 s1, 0x12000
	s_nop 0
	v_addc_co_u32_e32 v7, vcc, 0, v3, vcc
	v_add_co_u32_e32 v8, vcc, s1, v2
	s_mov_b32 s1, 0x14000
	s_nop 0
	v_addc_co_u32_e32 v9, vcc, 0, v3, vcc
	global_load_dwordx4 v[98:101], v[6:7], off sc0 nt
	global_load_dwordx4 v[102:105], v[8:9], off sc0 nt
	v_add_co_u32_e32 v6, vcc, s1, v2
	s_mov_b32 s1, 0x16000
	s_nop 0
	v_addc_co_u32_e32 v7, vcc, 0, v3, vcc
	v_add_co_u32_e32 v8, vcc, s1, v2
	s_mov_b32 s1, 0x18000
	s_nop 0
	v_addc_co_u32_e32 v9, vcc, 0, v3, vcc
	global_load_dwordx4 v[114:117], v[6:7], off sc0 nt
	global_load_dwordx4 v[110:113], v[8:9], off sc0 nt
	v_add_co_u32_e32 v6, vcc, s1, v2
	s_mov_b32 s1, 0x1a000
	s_nop 0
	v_addc_co_u32_e32 v7, vcc, 0, v3, vcc
	v_add_co_u32_e32 v8, vcc, s1, v2
	s_mov_b32 s1, 0x1c000
	s_nop 0
	v_addc_co_u32_e32 v9, vcc, 0, v3, vcc
	global_load_dwordx4 v[118:121], v[6:7], off sc0 nt
	global_load_dwordx4 v[122:125], v[8:9], off sc0 nt
	v_add_co_u32_e32 v6, vcc, s1, v2
	s_mov_b32 s1, 0x1e000
	s_nop 0
	v_addc_co_u32_e32 v7, vcc, 0, v3, vcc
	v_add_co_u32_e32 v8, vcc, s1, v2
	s_mov_b32 s1, 0x200000
	s_nop 0
	v_addc_co_u32_e32 v9, vcc, 0, v3, vcc
	v_add_co_u32_e32 v14, vcc, s1, v2
	s_mov_b32 s1, 0x202000
	s_nop 0
	v_addc_co_u32_e32 v15, vcc, 0, v3, vcc
	v_add_co_u32_e32 v16, vcc, s1, v2
	s_mov_b32 s1, 0x204000
	s_nop 0
	v_addc_co_u32_e32 v17, vcc, 0, v3, vcc
	v_add_co_u32_e32 v22, vcc, s1, v2
	s_mov_b32 s1, 0x206000
	s_nop 0
	v_addc_co_u32_e32 v23, vcc, 0, v3, vcc
	v_add_co_u32_e32 v24, vcc, s1, v2
	s_mov_b32 s1, 0x208000
	s_nop 0
	v_addc_co_u32_e32 v25, vcc, 0, v3, vcc
	v_add_co_u32_e32 v30, vcc, s1, v2
	s_mov_b32 s1, 0x20a000
	s_nop 0
	v_addc_co_u32_e32 v31, vcc, 0, v3, vcc
	v_add_co_u32_e32 v32, vcc, s1, v2
	s_mov_b32 s1, 0x20c000
	s_nop 0
	v_addc_co_u32_e32 v33, vcc, 0, v3, vcc
	s_waitcnt vmcnt(0)
	v_add_co_u32_e32 v46, vcc, s1, v2
	s_mov_b32 s1, 0x20e000
	s_nop 0
	v_addc_co_u32_e32 v47, vcc, 0, v3, vcc
	v_add_co_u32_e32 v48, vcc, s1, v2
	s_mov_b32 s1, 0x210000
	s_nop 0
	v_addc_co_u32_e32 v49, vcc, 0, v3, vcc
	v_add_co_u32_e32 v62, vcc, s1, v2
	s_mov_b32 s1, 0x212000
	s_nop 0
	v_addc_co_u32_e32 v63, vcc, 0, v3, vcc
	v_add_co_u32_e32 v64, vcc, s1, v2
	s_mov_b32 s1, 0x214000
	s_nop 0
	v_addc_co_u32_e32 v65, vcc, 0, v3, vcc
	v_add_co_u32_e32 v78, vcc, s1, v2
	s_mov_b32 s1, 0x216000
	s_nop 0
	v_addc_co_u32_e32 v79, vcc, 0, v3, vcc
	v_add_co_u32_e32 v80, vcc, s1, v2
	s_mov_b32 s1, 0x218000
	s_nop 0
	v_addc_co_u32_e32 v81, vcc, 0, v3, vcc
	global_load_dwordx4 v[130:133], v[6:7], off sc0 nt
	global_load_dwordx4 v[126:129], v[8:9], off sc0 nt
	s_nop 0
	global_load_dwordx4 v[6:9], v[14:15], off sc0 nt
	global_load_dwordx4 v[10:13], v[16:17], off sc0 nt
	global_load_dwordx4 v[18:21], v[22:23], off sc0 nt
	s_nop 0
	global_load_dwordx4 v[14:17], v[24:25], off sc0 nt
	s_nop 0
	global_load_dwordx4 v[22:25], v[30:31], off sc0 nt
	global_load_dwordx4 v[26:29], v[32:33], off sc0 nt
	global_load_dwordx4 v[42:45], v[46:47], off sc0 nt
	s_nop 0
	global_load_dwordx4 v[30:33], v[48:49], off sc0 nt
	s_nop 0
	global_load_dwordx4 v[46:49], v[62:63], off sc0 nt
	global_load_dwordx4 v[54:57], v[64:65], off sc0 nt
	global_load_dwordx4 v[74:77], v[78:79], off sc0 nt
	s_nop 0
	global_load_dwordx4 v[62:65], v[80:81], off sc0 nt
	v_add_co_u32_e32 v78, vcc, s1, v2
	s_mov_b32 s1, 0x21a000
	s_nop 0
	v_addc_co_u32_e32 v79, vcc, 0, v3, vcc
	v_add_co_u32_e32 v86, vcc, s1, v2
	s_mov_b32 s1, 0x21c000
	s_nop 0
	v_addc_co_u32_e32 v87, vcc, 0, v3, vcc
	v_add_co_u32_e32 v90, vcc, s1, v2
	s_mov_b32 s1, 0x21e000
	s_nop 0
	v_addc_co_u32_e32 v91, vcc, 0, v3, vcc
	v_add_co_u32_e32 v92, vcc, s1, v2
	global_load_dwordx4 v[78:81], v[78:79], off sc0 nt
	s_nop 0
	global_load_dwordx4 v[86:89], v[86:87], off sc0 nt
	v_addc_co_u32_e32 v93, vcc, 0, v3, vcc
	global_load_dwordx4 v[106:109], v[90:91], off sc0 nt
	s_nop 0
	global_load_dwordx4 v[90:93], v[92:93], off sc0 nt
	v_readlane_b32 s13, v254, 5
	v_readlane_b32 s14, v254, 6
	v_readlane_b32 s15, v254, 7
	v_readlane_b32 s16, v254, 8
	v_readlane_b32 s17, v254, 9
	s_add_i32 s2, s0, 0
	v_mul_f32_e32 v4, 0x43800000, v34
	v_mul_f32_e32 v34, 0x43800000, v38
	s_mov_b32 s0, 0xc3e00000
	v_mov_b32_e32 v1, 0x43e00000
	v_med3_f32 v4, v4, s0, v1
	v_med3_f32 v34, v34, s0, v1
	v_mov_b32_e32 v136, v5
	v_cvt_pk_fp8_f32 v136, v4, v34
	v_mul_f32_e32 v38, 0x43800000, v58
	v_mul_f32_e32 v4, 0x43800000, v50
	v_med3_f32 v34, v38, s0, v1
	v_med3_f32 v4, v4, s0, v1
	v_cvt_pk_fp8_f32 v136, v34, v4 op_sel:[0,0,1]
	v_mul_f32_e32 v4, 0x43800000, v66
	v_mul_f32_e32 v34, 0x43800000, v70
	v_med3_f32 v4, v4, s0, v1
	v_med3_f32 v34, v34, s0, v1
	v_mov_b32_e32 v137, v5
	v_cvt_pk_fp8_f32 v137, v4, v34
	v_mul_f32_e32 v38, 0x43800000, v94
	v_mul_f32_e32 v4, 0x43800000, v82
	v_med3_f32 v34, v38, s0, v1
	v_med3_f32 v4, v4, s0, v1
	v_cvt_pk_fp8_f32 v137, v34, v4 op_sel:[0,0,1]
	v_mul_f32_e32 v4, 0x43800000, v98
	v_mul_f32_e32 v34, 0x43800000, v102
	v_med3_f32 v4, v4, s0, v1
	v_med3_f32 v34, v34, s0, v1
	v_mov_b32_e32 v138, v5
	v_cvt_pk_fp8_f32 v138, v4, v34
	v_mul_f32_e32 v38, 0x43800000, v114
	v_mul_f32_e32 v4, 0x43800000, v110
	v_med3_f32 v34, v38, s0, v1
	v_med3_f32 v4, v4, s0, v1
	v_cvt_pk_fp8_f32 v138, v34, v4 op_sel:[0,0,1]
	v_mul_f32_e32 v4, 0x43800000, v118
	v_mul_f32_e32 v34, 0x43800000, v122
	v_med3_f32 v4, v4, s0, v1
	v_med3_f32 v34, v34, s0, v1
	v_mov_b32_e32 v139, v5
	v_cvt_pk_fp8_f32 v139, v4, v34
	s_waitcnt vmcnt(17)
	v_mul_f32_e32 v38, 0x43800000, v130
	s_waitcnt vmcnt(16)
	v_mul_f32_e32 v4, 0x43800000, v126
	v_med3_f32 v34, v38, s0, v1
	v_med3_f32 v4, v4, s0, v1
	v_cvt_pk_fp8_f32 v139, v34, v4 op_sel:[0,0,1]
	v_mul_u32_u24_e32 v4, 0x110, v140
	v_add3_u32 v166, s2, v135, v4
	v_mul_f32_e32 v4, 0x43800000, v35
	v_mul_f32_e32 v34, 0x43800000, v39
	v_med3_f32 v4, v4, s0, v1
	v_med3_f32 v34, v34, s0, v1
	v_mov_b32_e32 v140, v5
	v_cvt_pk_fp8_f32 v140, v4, v34
	v_mul_f32_e32 v35, 0x43800000, v59
	v_mul_f32_e32 v4, 0x43800000, v51
	v_med3_f32 v34, v35, s0, v1
	v_med3_f32 v4, v4, s0, v1
	v_cvt_pk_fp8_f32 v140, v34, v4 op_sel:[0,0,1]
	v_mul_f32_e32 v4, 0x43800000, v67
	v_mul_f32_e32 v34, 0x43800000, v71
	v_med3_f32 v4, v4, s0, v1
	v_med3_f32 v34, v34, s0, v1
	v_mov_b32_e32 v141, v5
	v_cvt_pk_fp8_f32 v141, v4, v34
	v_mul_f32_e32 v35, 0x43800000, v95
	v_mul_f32_e32 v4, 0x43800000, v83
	v_med3_f32 v34, v35, s0, v1
	v_med3_f32 v4, v4, s0, v1
	v_cvt_pk_fp8_f32 v141, v34, v4 op_sel:[0,0,1]
	v_mul_f32_e32 v4, 0x43800000, v99
	v_mul_f32_e32 v34, 0x43800000, v103
	v_med3_f32 v4, v4, s0, v1
	v_med3_f32 v34, v34, s0, v1
	v_mov_b32_e32 v142, v5
	v_cvt_pk_fp8_f32 v142, v4, v34
	v_mul_f32_e32 v35, 0x43800000, v115
	v_mul_f32_e32 v4, 0x43800000, v111
	v_med3_f32 v34, v35, s0, v1
	v_med3_f32 v4, v4, s0, v1
	v_cvt_pk_fp8_f32 v142, v34, v4 op_sel:[0,0,1]
	v_mul_f32_e32 v4, 0x43800000, v119
	v_mul_f32_e32 v34, 0x43800000, v123
	v_med3_f32 v4, v4, s0, v1
	v_med3_f32 v34, v34, s0, v1
	v_mov_b32_e32 v143, v5
	v_cvt_pk_fp8_f32 v143, v4, v34
	v_mul_f32_e32 v35, 0x43800000, v131
	v_mul_f32_e32 v4, 0x43800000, v127
	v_med3_f32 v34, v35, s0, v1
	v_med3_f32 v4, v4, s0, v1
	v_cvt_pk_fp8_f32 v143, v34, v4 op_sel:[0,0,1]
	v_mul_f32_e32 v4, 0x43800000, v36
	v_mul_f32_e32 v34, 0x43800000, v40
	v_med3_f32 v4, v4, s0, v1
	v_med3_f32 v34, v34, s0, v1
	v_mov_b32_e32 v144, v5
	v_cvt_pk_fp8_f32 v144, v4, v34
	v_mul_f32_e32 v35, 0x43800000, v60
	v_mul_f32_e32 v4, 0x43800000, v52
	v_med3_f32 v34, v35, s0, v1
	v_med3_f32 v4, v4, s0, v1
	v_cvt_pk_fp8_f32 v144, v34, v4 op_sel:[0,0,1]
	v_mul_f32_e32 v4, 0x43800000, v68
	v_mul_f32_e32 v34, 0x43800000, v72
	v_med3_f32 v4, v4, s0, v1
	v_med3_f32 v34, v34, s0, v1
	v_mov_b32_e32 v145, v5
	v_cvt_pk_fp8_f32 v145, v4, v34
	v_mul_f32_e32 v35, 0x43800000, v96
	v_mul_f32_e32 v4, 0x43800000, v84
	v_med3_f32 v34, v35, s0, v1
	v_med3_f32 v4, v4, s0, v1
	v_cvt_pk_fp8_f32 v145, v34, v4 op_sel:[0,0,1]
	v_mul_f32_e32 v4, 0x43800000, v100
	v_mul_f32_e32 v34, 0x43800000, v104
	v_med3_f32 v4, v4, s0, v1
	v_med3_f32 v34, v34, s0, v1
	v_mov_b32_e32 v146, v5
	v_cvt_pk_fp8_f32 v146, v4, v34
	v_mul_f32_e32 v35, 0x43800000, v116
	v_mul_f32_e32 v4, 0x43800000, v112
	v_med3_f32 v34, v35, s0, v1
	v_med3_f32 v4, v4, s0, v1
	v_cvt_pk_fp8_f32 v146, v34, v4 op_sel:[0,0,1]
	v_mul_f32_e32 v4, 0x43800000, v120
	v_mul_f32_e32 v34, 0x43800000, v124
	v_med3_f32 v4, v4, s0, v1
	v_med3_f32 v34, v34, s0, v1
	v_mov_b32_e32 v147, v5
	v_cvt_pk_fp8_f32 v147, v4, v34
	v_mul_f32_e32 v35, 0x43800000, v132
	v_mul_f32_e32 v4, 0x43800000, v128
	v_med3_f32 v34, v35, s0, v1
	v_med3_f32 v4, v4, s0, v1
	v_cvt_pk_fp8_f32 v147, v34, v4 op_sel:[0,0,1]
	v_mul_f32_e32 v4, 0x43800000, v37
	v_mul_f32_e32 v34, 0x43800000, v41
	v_med3_f32 v4, v4, s0, v1
	v_med3_f32 v36, v34, s0, v1
	v_mov_b32_e32 v34, v5
	v_cvt_pk_fp8_f32 v34, v4, v36
	v_mul_f32_e32 v35, 0x43800000, v61
	v_mul_f32_e32 v4, 0x43800000, v53
	v_med3_f32 v35, v35, s0, v1
	v_med3_f32 v4, v4, s0, v1
	v_cvt_pk_fp8_f32 v34, v35, v4 op_sel:[0,0,1]
	v_mul_f32_e32 v4, 0x43800000, v69
	v_mul_f32_e32 v35, 0x43800000, v73
	v_med3_f32 v4, v4, s0, v1
	v_med3_f32 v37, v35, s0, v1
	v_mov_b32_e32 v35, v5
	v_cvt_pk_fp8_f32 v35, v4, v37
	v_mul_f32_e32 v36, 0x43800000, v97
	v_mul_f32_e32 v4, 0x43800000, v85
	v_med3_f32 v36, v36, s0, v1
	v_med3_f32 v4, v4, s0, v1
	v_cvt_pk_fp8_f32 v35, v36, v4 op_sel:[0,0,1]
	v_mul_f32_e32 v4, 0x43800000, v101
	v_mul_f32_e32 v36, 0x43800000, v105
	v_med3_f32 v4, v4, s0, v1
	v_med3_f32 v38, v36, s0, v1
	v_mov_b32_e32 v36, v5
	v_cvt_pk_fp8_f32 v36, v4, v38
	v_mul_f32_e32 v37, 0x43800000, v117
	v_mul_f32_e32 v4, 0x43800000, v113
	v_med3_f32 v37, v37, s0, v1
	v_med3_f32 v4, v4, s0, v1
	v_cvt_pk_fp8_f32 v36, v37, v4 op_sel:[0,0,1]
	v_mul_f32_e32 v4, 0x43800000, v121
	v_mul_f32_e32 v37, 0x43800000, v125
	v_med3_f32 v4, v4, s0, v1
	v_med3_f32 v39, v37, s0, v1
	v_mov_b32_e32 v37, v5
	v_cvt_pk_fp8_f32 v37, v4, v39
	v_mul_f32_e32 v38, 0x43800000, v133
	v_mul_f32_e32 v4, 0x43800000, v129
	v_med3_f32 v38, v38, s0, v1
	v_med3_f32 v4, v4, s0, v1
	v_cvt_pk_fp8_f32 v37, v38, v4 op_sel:[0,0,1]
	ds_write_b128 v166, v[136:139]
	ds_write_b128 v166, v[140:143] offset:272
	ds_write_b128 v166, v[144:147] offset:544
	ds_write_b128 v166, v[34:37] offset:816
	v_add_u32_e32 v34, 0x200, v134
	v_ashrrev_i32_e32 v140, 4, v34
	v_add_u32_e32 v34, 0x400, v134
	v_ashrrev_i32_e32 v144, 4, v34
	v_add_u32_e32 v34, 0x600, v134
	v_ashrrev_i32_e32 v136, 4, v134
	v_ashrrev_i32_e32 v148, 4, v34
	v_lshlrev_b32_e32 v4, 4, v134
	v_ashrrev_i32_e32 v137, 31, v136
	v_ashrrev_i32_e32 v141, 31, v140
	v_ashrrev_i32_e32 v145, 31, v144
	v_ashrrev_i32_e32 v149, 31, v148
	s_movk_i32 s1, 0x110
	s_waitcnt lgkmcnt(0)
	s_barrier
	v_and_b32_e32 v4, 0xf0, v4
	v_lshlrev_b64 v[138:139], 11, v[136:137]
	v_lshlrev_b64 v[142:143], 11, v[140:141]
	v_lshlrev_b64 v[146:147], 11, v[144:145]
	v_lshlrev_b64 v[164:165], 11, v[148:149]
	s_mov_b32 s2, 0x400000
	v_add_co_u32_e32 v34, vcc, s2, v2
	s_mov_b32 s2, 0x402000
	s_nop 0
	v_addc_co_u32_e32 v35, vcc, 0, v3, vcc
	v_add_co_u32_e32 v38, vcc, s2, v2
	s_mov_b32 s2, 0x404000
	s_nop 0
	v_addc_co_u32_e32 v39, vcc, 0, v3, vcc
	v_add_co_u32_e32 v66, vcc, s2, v2
	s_mov_b32 s2, 0x406000
	s_nop 0
	v_addc_co_u32_e32 v67, vcc, 0, v3, vcc
	v_add_co_u32_e32 v68, vcc, s2, v2
	s_mov_b32 s2, 0x408000
	s_nop 0
	v_addc_co_u32_e32 v69, vcc, 0, v3, vcc
	v_add_co_u32_e32 v82, vcc, s2, v2
	s_mov_b32 s2, 0x40a000
	s_nop 0
	v_addc_co_u32_e32 v83, vcc, 0, v3, vcc
	v_add_co_u32_e32 v84, vcc, s2, v2
	s_mov_b32 s2, 0x40c000
	s_nop 0
	v_addc_co_u32_e32 v85, vcc, 0, v3, vcc
	v_add_co_u32_e32 v98, vcc, s2, v2
	s_mov_b32 s2, 0x40e000
	s_nop 0
	v_addc_co_u32_e32 v99, vcc, 0, v3, vcc
	v_add_co_u32_e32 v100, vcc, s2, v2
	s_mov_b32 s2, 0x410000
	s_nop 0
	v_addc_co_u32_e32 v101, vcc, 0, v3, vcc
	v_add_co_u32_e32 v110, vcc, s2, v2
	s_mov_b32 s2, 0x412000
	s_nop 0
	v_addc_co_u32_e32 v111, vcc, 0, v3, vcc
	v_add_co_u32_e32 v112, vcc, s2, v2
	s_mov_b32 s2, 0x414000
	s_nop 0
	v_addc_co_u32_e32 v113, vcc, 0, v3, vcc
	global_load_dwordx4 v[34:37], v[34:35], off sc0 nt
	s_nop 0
	global_load_dwordx4 v[38:41], v[38:39], off sc0 nt
	s_nop 0
	global_load_dwordx4 v[58:61], v[66:67], off sc0 nt
	global_load_dwordx4 v[50:53], v[68:69], off sc0 nt
	s_nop 0
	global_load_dwordx4 v[66:69], v[82:83], off sc0 nt
	global_load_dwordx4 v[70:73], v[84:85], off sc0 nt
	global_load_dwordx4 v[94:97], v[98:99], off sc0 nt
	s_nop 0
	global_load_dwordx4 v[82:85], v[100:101], off sc0 nt
	s_nop 0
	global_load_dwordx4 v[98:101], v[110:111], off sc0 nt
	global_load_dwordx4 v[102:105], v[112:113], off sc0 nt
	v_add_co_u32_e32 v110, vcc, s2, v2
	s_mov_b32 s2, 0x416000
	s_nop 0
	v_addc_co_u32_e32 v111, vcc, 0, v3, vcc
	v_add_co_u32_e32 v112, vcc, s2, v2
	s_mov_b32 s2, 0x418000
	s_nop 0
	v_addc_co_u32_e32 v113, vcc, 0, v3, vcc
	v_add_co_u32_e32 v118, vcc, s2, v2
	s_mov_b32 s2, 0x41a000
	s_nop 0
	v_addc_co_u32_e32 v119, vcc, 0, v3, vcc
	v_add_co_u32_e32 v122, vcc, s2, v2
	s_mov_b32 s2, 0x41c000
	s_nop 0
	v_addc_co_u32_e32 v123, vcc, 0, v3, vcc
	v_add_co_u32_e32 v126, vcc, s2, v2
	s_mov_b32 s2, 0x41e000
	s_nop 0
	v_addc_co_u32_e32 v127, vcc, 0, v3, vcc
	v_add_co_u32_e32 v128, vcc, s2, v2
	global_load_dwordx4 v[114:117], v[110:111], off sc0 nt
	s_nop 0
	global_load_dwordx4 v[110:113], v[112:113], off sc0 nt
	v_addc_co_u32_e32 v129, vcc, 0, v3, vcc
	global_load_dwordx4 v[118:121], v[118:119], off sc0 nt
	s_nop 0
	global_load_dwordx4 v[122:125], v[122:123], off sc0 nt
	s_nop 0
	global_load_dwordx4 v[130:133], v[126:127], off sc0 nt
	s_nop 0
	global_load_dwordx4 v[126:129], v[128:129], off sc0 nt
	v_add_u32_e32 v160, 0, v4
	v_lshl_add_u64 v[134:135], s[6:7], 0, v[4:5]
	s_mov_b64 s[2:3], 0x60000000
	v_lshl_add_u64 v[168:169], v[134:135], 0, s[2:3]
	v_mad_u64_u32 v[154:155], s[2:3], v136, s1, v[160:161]
	ds_read_b128 v[134:137], v154
	v_lshl_add_u64 v[150:151], v[168:169], 0, v[138:139]
	v_mad_u64_u32 v[156:157], s[2:3], v140, s1, v[160:161]
	v_mad_u64_u32 v[158:159], s[2:3], v144, s1, v[160:161]
	v_mad_u64_u32 v[162:163], s[2:3], v148, s1, v[160:161]
	ds_read_b128 v[138:141], v156
	s_waitcnt lgkmcnt(1)
	global_store_dwordx4 v[150:151], v[134:137], off nt
	v_lshl_add_u64 v[152:153], v[168:169], 0, v[142:143]
	ds_read_b128 v[134:137], v158
	ds_read_b128 v[142:145], v162
	v_lshl_add_u64 v[160:161], v[168:169], 0, v[146:147]
	v_lshl_add_u64 v[164:165], v[168:169], 0, v[164:165]
	s_waitcnt lgkmcnt(2)
	global_store_dwordx4 v[152:153], v[138:141], off nt
	s_waitcnt lgkmcnt(1)
	global_store_dwordx4 v[160:161], v[134:137], off nt
	s_waitcnt lgkmcnt(0)
	global_store_dwordx4 v[164:165], v[142:145], off nt
	s_waitcnt vmcnt(35)
	v_mul_f32_e32 v4, 0x43800000, v6
	s_waitcnt vmcnt(34)
	v_mul_f32_e32 v6, 0x43800000, v10
	v_med3_f32 v4, v4, s0, v1
	v_med3_f32 v6, v6, s0, v1
	v_mov_b32_e32 v134, v5
	v_cvt_pk_fp8_f32 v134, v4, v6
	s_waitcnt vmcnt(33)
	v_mul_f32_e32 v10, 0x43800000, v18
	s_waitcnt vmcnt(32)
	v_mul_f32_e32 v4, 0x43800000, v14
	v_med3_f32 v6, v10, s0, v1
	v_med3_f32 v4, v4, s0, v1
	v_cvt_pk_fp8_f32 v134, v6, v4 op_sel:[0,0,1]
	s_waitcnt vmcnt(31)
	v_mul_f32_e32 v4, 0x43800000, v22
	s_waitcnt vmcnt(30)
	v_mul_f32_e32 v6, 0x43800000, v26
	v_med3_f32 v4, v4, s0, v1
	v_med3_f32 v6, v6, s0, v1
	v_mov_b32_e32 v135, v5
	v_cvt_pk_fp8_f32 v135, v4, v6
	s_waitcnt vmcnt(29)
	v_mul_f32_e32 v10, 0x43800000, v42
	s_waitcnt vmcnt(28)
	v_mul_f32_e32 v4, 0x43800000, v30
	v_med3_f32 v6, v10, s0, v1
	v_med3_f32 v4, v4, s0, v1
	v_cvt_pk_fp8_f32 v135, v6, v4 op_sel:[0,0,1]
	s_waitcnt vmcnt(27)
	v_mul_f32_e32 v4, 0x43800000, v46
	s_waitcnt vmcnt(26)
	v_mul_f32_e32 v6, 0x43800000, v54
	v_med3_f32 v4, v4, s0, v1
	v_med3_f32 v6, v6, s0, v1
	v_mov_b32_e32 v136, v5
	v_cvt_pk_fp8_f32 v136, v4, v6
	s_waitcnt vmcnt(25)
	v_mul_f32_e32 v10, 0x43800000, v74
	s_waitcnt vmcnt(24)
	v_mul_f32_e32 v4, 0x43800000, v62
	v_med3_f32 v6, v10, s0, v1
	v_med3_f32 v4, v4, s0, v1
	v_cvt_pk_fp8_f32 v136, v6, v4 op_sel:[0,0,1]
	s_waitcnt vmcnt(23)
	v_mul_f32_e32 v4, 0x43800000, v78
	s_waitcnt vmcnt(22)
	v_mul_f32_e32 v6, 0x43800000, v86
	v_med3_f32 v4, v4, s0, v1
	v_med3_f32 v6, v6, s0, v1
	v_mov_b32_e32 v137, v5
	v_cvt_pk_fp8_f32 v137, v4, v6
	s_waitcnt vmcnt(21)
	v_mul_f32_e32 v10, 0x43800000, v106
	s_waitcnt vmcnt(20)
	v_mul_f32_e32 v4, 0x43800000, v90
	v_med3_f32 v6, v10, s0, v1
	v_med3_f32 v4, v4, s0, v1
	v_cvt_pk_fp8_f32 v137, v6, v4 op_sel:[0,0,1]
	v_mul_f32_e32 v4, 0x43800000, v7
	v_mul_f32_e32 v6, 0x43800000, v11
	v_med3_f32 v4, v4, s0, v1
	v_med3_f32 v6, v6, s0, v1
	v_mov_b32_e32 v138, v5
	v_cvt_pk_fp8_f32 v138, v4, v6
	v_mul_f32_e32 v7, 0x43800000, v19
	v_mul_f32_e32 v4, 0x43800000, v15
	v_med3_f32 v6, v7, s0, v1
	v_med3_f32 v4, v4, s0, v1
	v_cvt_pk_fp8_f32 v138, v6, v4 op_sel:[0,0,1]
	v_mul_f32_e32 v4, 0x43800000, v23
	v_mul_f32_e32 v6, 0x43800000, v27
	v_med3_f32 v4, v4, s0, v1
	v_med3_f32 v6, v6, s0, v1
	v_mov_b32_e32 v139, v5
	v_cvt_pk_fp8_f32 v139, v4, v6
	v_mul_f32_e32 v7, 0x43800000, v43
	v_mul_f32_e32 v4, 0x43800000, v31
	v_med3_f32 v6, v7, s0, v1
	v_med3_f32 v4, v4, s0, v1
	v_cvt_pk_fp8_f32 v139, v6, v4 op_sel:[0,0,1]
	v_mul_f32_e32 v4, 0x43800000, v47
	v_mul_f32_e32 v6, 0x43800000, v55
	v_med3_f32 v4, v4, s0, v1
	v_med3_f32 v6, v6, s0, v1
	v_mov_b32_e32 v140, v5
	v_cvt_pk_fp8_f32 v140, v4, v6
	v_mul_f32_e32 v7, 0x43800000, v75
	v_mul_f32_e32 v4, 0x43800000, v63
	v_med3_f32 v6, v7, s0, v1
	v_med3_f32 v4, v4, s0, v1
	v_cvt_pk_fp8_f32 v140, v6, v4 op_sel:[0,0,1]
	v_mul_f32_e32 v4, 0x43800000, v79
	v_mul_f32_e32 v6, 0x43800000, v87
	v_med3_f32 v4, v4, s0, v1
	v_med3_f32 v6, v6, s0, v1
	v_mov_b32_e32 v141, v5
	v_cvt_pk_fp8_f32 v141, v4, v6
	v_mul_f32_e32 v7, 0x43800000, v107
	v_mul_f32_e32 v4, 0x43800000, v91
	v_med3_f32 v6, v7, s0, v1
	v_med3_f32 v4, v4, s0, v1
	v_cvt_pk_fp8_f32 v141, v6, v4 op_sel:[0,0,1]
	v_mul_f32_e32 v4, 0x43800000, v8
	v_mul_f32_e32 v6, 0x43800000, v12
	v_med3_f32 v4, v4, s0, v1
	v_med3_f32 v6, v6, s0, v1
	v_mov_b32_e32 v142, v5
	v_cvt_pk_fp8_f32 v142, v4, v6
	v_mul_f32_e32 v7, 0x43800000, v20
	v_mul_f32_e32 v4, 0x43800000, v16
	v_med3_f32 v6, v7, s0, v1
	v_med3_f32 v4, v4, s0, v1
	v_cvt_pk_fp8_f32 v142, v6, v4 op_sel:[0,0,1]
	v_mul_f32_e32 v4, 0x43800000, v24
	v_mul_f32_e32 v6, 0x43800000, v28
	v_med3_f32 v4, v4, s0, v1
	v_med3_f32 v6, v6, s0, v1
	v_mov_b32_e32 v143, v5
	v_cvt_pk_fp8_f32 v143, v4, v6
	v_mul_f32_e32 v7, 0x43800000, v44
	v_mul_f32_e32 v4, 0x43800000, v32
	v_med3_f32 v6, v7, s0, v1
	v_med3_f32 v4, v4, s0, v1
	v_cvt_pk_fp8_f32 v143, v6, v4 op_sel:[0,0,1]
	v_mul_f32_e32 v4, 0x43800000, v48
	v_mul_f32_e32 v6, 0x43800000, v56
	v_med3_f32 v4, v4, s0, v1
	v_med3_f32 v6, v6, s0, v1
	v_mov_b32_e32 v144, v5
	v_cvt_pk_fp8_f32 v144, v4, v6
	v_mul_f32_e32 v7, 0x43800000, v76
	v_mul_f32_e32 v4, 0x43800000, v64
	v_med3_f32 v6, v7, s0, v1
	v_med3_f32 v4, v4, s0, v1
	v_cvt_pk_fp8_f32 v144, v6, v4 op_sel:[0,0,1]
	v_mul_f32_e32 v4, 0x43800000, v80
	v_mul_f32_e32 v6, 0x43800000, v88
	v_med3_f32 v4, v4, s0, v1
	v_med3_f32 v6, v6, s0, v1
	v_mov_b32_e32 v145, v5
	v_cvt_pk_fp8_f32 v145, v4, v6
	v_mul_f32_e32 v7, 0x43800000, v108
	v_mul_f32_e32 v4, 0x43800000, v92
	v_med3_f32 v6, v7, s0, v1
	v_med3_f32 v4, v4, s0, v1
	v_cvt_pk_fp8_f32 v145, v6, v4 op_sel:[0,0,1]
	v_mul_f32_e32 v4, 0x43800000, v9
	v_mul_f32_e32 v6, 0x43800000, v13
	v_med3_f32 v4, v4, s0, v1
	v_med3_f32 v8, v6, s0, v1
	v_mov_b32_e32 v6, v5
	v_cvt_pk_fp8_f32 v6, v4, v8
	v_mul_f32_e32 v7, 0x43800000, v21
	v_mul_f32_e32 v4, 0x43800000, v17
	v_med3_f32 v7, v7, s0, v1
	v_med3_f32 v4, v4, s0, v1
	v_cvt_pk_fp8_f32 v6, v7, v4 op_sel:[0,0,1]
	v_mul_f32_e32 v4, 0x43800000, v25
	v_mul_f32_e32 v7, 0x43800000, v29
	v_med3_f32 v4, v4, s0, v1
	v_med3_f32 v9, v7, s0, v1
	v_mov_b32_e32 v7, v5
	v_cvt_pk_fp8_f32 v7, v4, v9
	v_mul_f32_e32 v8, 0x43800000, v45
	v_mul_f32_e32 v4, 0x43800000, v33
	v_med3_f32 v8, v8, s0, v1
	v_med3_f32 v4, v4, s0, v1
	v_cvt_pk_fp8_f32 v7, v8, v4 op_sel:[0,0,1]
	v_mul_f32_e32 v4, 0x43800000, v49
	v_mul_f32_e32 v8, 0x43800000, v57
	v_med3_f32 v4, v4, s0, v1
	v_med3_f32 v10, v8, s0, v1
	v_mov_b32_e32 v8, v5
	v_cvt_pk_fp8_f32 v8, v4, v10
	v_mul_f32_e32 v9, 0x43800000, v77
	v_mul_f32_e32 v4, 0x43800000, v65
	v_med3_f32 v9, v9, s0, v1
	v_med3_f32 v4, v4, s0, v1
	v_cvt_pk_fp8_f32 v8, v9, v4 op_sel:[0,0,1]
	v_mul_f32_e32 v4, 0x43800000, v81
	v_mul_f32_e32 v9, 0x43800000, v89
	v_med3_f32 v4, v4, s0, v1
	v_med3_f32 v11, v9, s0, v1
	v_mov_b32_e32 v9, v5
	v_cvt_pk_fp8_f32 v9, v4, v11
	v_mul_f32_e32 v10, 0x43800000, v109
	v_mul_f32_e32 v4, 0x43800000, v93
	v_med3_f32 v10, v10, s0, v1
	v_med3_f32 v4, v4, s0, v1
	v_cvt_pk_fp8_f32 v9, v10, v4 op_sel:[0,0,1]
	ds_write_b128 v166, v[134:137] offset:34816
	ds_write_b128 v166, v[138:141] offset:35088
	ds_write_b128 v166, v[142:145] offset:35360
	ds_write_b128 v166, v[6:9] offset:35632
	s_waitcnt lgkmcnt(0)
	s_barrier
	s_mov_b32 s1, 0x600000
	v_add_co_u32_e32 v6, vcc, s1, v2
	s_mov_b32 s1, 0x602000
	s_nop 0
	v_addc_co_u32_e32 v7, vcc, 0, v3, vcc
	v_add_co_u32_e32 v10, vcc, s1, v2
	s_mov_b32 s1, 0x604000
	s_nop 0
	v_addc_co_u32_e32 v11, vcc, 0, v3, vcc
	global_load_dwordx4 v[6:9], v[6:7], off sc0 nt
	s_nop 0
	global_load_dwordx4 v[14:17], v[10:11], off sc0 nt
	v_add_co_u32_e32 v10, vcc, s1, v2
	s_mov_b32 s1, 0x606000
	s_nop 0
	v_addc_co_u32_e32 v11, vcc, 0, v3, vcc
	v_add_co_u32_e32 v12, vcc, s1, v2
	s_mov_b32 s1, 0x608000
	s_nop 0
	v_addc_co_u32_e32 v13, vcc, 0, v3, vcc
	global_load_dwordx4 v[30:33], v[10:11], off sc0 nt
	global_load_dwordx4 v[22:25], v[12:13], off sc0 nt
	v_add_co_u32_e32 v10, vcc, s1, v2
	s_mov_b32 s1, 0x60a000
	s_nop 0
	v_addc_co_u32_e32 v11, vcc, 0, v3, vcc
	v_add_co_u32_e32 v12, vcc, s1, v2
	s_mov_b32 s1, 0x60c000
	s_nop 0
	v_addc_co_u32_e32 v13, vcc, 0, v3, vcc
	global_load_dwordx4 v[42:45], v[10:11], off sc0 nt
	global_load_dwordx4 v[46:49], v[12:13], off sc0 nt
	v_add_co_u32_e32 v10, vcc, s1, v2
	s_mov_b32 s1, 0x60e000
	s_nop 0
	v_addc_co_u32_e32 v11, vcc, 0, v3, vcc
	v_add_co_u32_e32 v12, vcc, s1, v2
	s_mov_b32 s1, 0x610000
	s_nop 0
	v_addc_co_u32_e32 v13, vcc, 0, v3, vcc
	global_load_dwordx4 v[62:65], v[10:11], off sc0 nt
	global_load_dwordx4 v[54:57], v[12:13], off sc0 nt
	v_add_co_u32_e32 v10, vcc, s1, v2
	s_mov_b32 s1, 0x612000
	s_nop 0
	v_addc_co_u32_e32 v11, vcc, 0, v3, vcc
	v_add_co_u32_e32 v12, vcc, s1, v2
	s_mov_b32 s1, 0x614000
	s_nop 0
	v_addc_co_u32_e32 v13, vcc, 0, v3, vcc
	global_load_dwordx4 v[74:77], v[10:11], off sc0 nt
	global_load_dwordx4 v[78:81], v[12:13], off sc0 nt
	v_add_co_u32_e32 v10, vcc, s1, v2
	s_mov_b32 s1, 0x616000
	s_nop 0
	v_addc_co_u32_e32 v11, vcc, 0, v3, vcc
	v_add_co_u32_e32 v12, vcc, s1, v2
	s_mov_b32 s1, 0x618000
	s_nop 0
	v_addc_co_u32_e32 v13, vcc, 0, v3, vcc
	global_load_dwordx4 v[106:109], v[10:11], off sc0 nt
	global_load_dwordx4 v[86:89], v[12:13], off sc0 nt
	v_add_co_u32_e32 v10, vcc, s1, v2
	s_mov_b32 s1, 0x61a000
	s_nop 0
	v_addc_co_u32_e32 v11, vcc, 0, v3, vcc
	v_add_co_u32_e32 v12, vcc, s1, v2
	s_mov_b32 s1, 0x61c000
	s_nop 0
	v_addc_co_u32_e32 v13, vcc, 0, v3, vcc
	global_load_dwordx4 v[134:137], v[10:11], off sc0 nt
	global_load_dwordx4 v[138:141], v[12:13], off sc0 nt
	v_add_co_u32_e32 v10, vcc, s1, v2
	s_mov_b32 s1, 0x61e000
	s_nop 0
	v_addc_co_u32_e32 v11, vcc, 0, v3, vcc
	v_add_co_u32_e32 v12, vcc, s1, v2
	s_nop 1
	v_addc_co_u32_e32 v13, vcc, 0, v3, vcc
	global_load_dwordx4 v[146:149], v[10:11], off sc0 nt
	global_load_dwordx4 v[142:145], v[12:13], off sc0 nt
	ds_read_b128 v[10:13], v154 offset:34816
	ds_read_b128 v[18:21], v156 offset:34816
	ds_read_b128 v[26:29], v158 offset:34816
	ds_read_b128 v[90:93], v162 offset:34816
	s_waitcnt lgkmcnt(3)
	global_store_dwordx4 v[150:151], v[10:13], off offset:256 nt
	s_waitcnt lgkmcnt(2)
	global_store_dwordx4 v[152:153], v[18:21], off offset:256 nt
	s_waitcnt lgkmcnt(1)
	global_store_dwordx4 v[160:161], v[26:29], off offset:256 nt
	s_waitcnt lgkmcnt(0)
	global_store_dwordx4 v[164:165], v[90:93], off offset:256 nt
	s_waitcnt vmcnt(39)
	v_mul_f32_e32 v4, 0x43800000, v34
	s_waitcnt vmcnt(38)
	v_mul_f32_e32 v10, 0x43800000, v38
	v_med3_f32 v4, v4, s0, v1
	v_med3_f32 v12, v10, s0, v1
	v_mov_b32_e32 v10, v5
	v_cvt_pk_fp8_f32 v10, v4, v12
	s_waitcnt vmcnt(37)
	v_mul_f32_e32 v11, 0x43800000, v58
	s_waitcnt vmcnt(36)
	v_mul_f32_e32 v4, 0x43800000, v50
	v_med3_f32 v11, v11, s0, v1
	v_med3_f32 v4, v4, s0, v1
	v_cvt_pk_fp8_f32 v10, v11, v4 op_sel:[0,0,1]
	s_waitcnt vmcnt(35)
	v_mul_f32_e32 v4, 0x43800000, v66
	s_waitcnt vmcnt(34)
	v_mul_f32_e32 v11, 0x43800000, v70
	v_med3_f32 v4, v4, s0, v1
	v_med3_f32 v13, v11, s0, v1
	v_mov_b32_e32 v11, v5
	v_cvt_pk_fp8_f32 v11, v4, v13
	s_waitcnt vmcnt(33)
	v_mul_f32_e32 v12, 0x43800000, v94
	s_waitcnt vmcnt(32)
	v_mul_f32_e32 v4, 0x43800000, v82
	v_med3_f32 v12, v12, s0, v1
	v_med3_f32 v4, v4, s0, v1
	v_cvt_pk_fp8_f32 v11, v12, v4 op_sel:[0,0,1]
	s_waitcnt vmcnt(31)
	v_mul_f32_e32 v4, 0x43800000, v98
	s_waitcnt vmcnt(30)
	v_mul_f32_e32 v12, 0x43800000, v102
	v_med3_f32 v4, v4, s0, v1
	v_med3_f32 v18, v12, s0, v1
	v_mov_b32_e32 v12, v5
	v_cvt_pk_fp8_f32 v12, v4, v18
	s_waitcnt vmcnt(29)
	v_mul_f32_e32 v13, 0x43800000, v114
	s_waitcnt vmcnt(28)
	v_mul_f32_e32 v4, 0x43800000, v110
	v_med3_f32 v13, v13, s0, v1
	v_med3_f32 v4, v4, s0, v1
	v_cvt_pk_fp8_f32 v12, v13, v4 op_sel:[0,0,1]
	s_waitcnt vmcnt(27)
	v_mul_f32_e32 v4, 0x43800000, v118
	s_waitcnt vmcnt(26)
	v_mul_f32_e32 v13, 0x43800000, v122
	v_med3_f32 v4, v4, s0, v1
	v_med3_f32 v19, v13, s0, v1
	v_mov_b32_e32 v13, v5
	v_cvt_pk_fp8_f32 v13, v4, v19
	s_waitcnt vmcnt(25)
	v_mul_f32_e32 v18, 0x43800000, v130
	s_waitcnt vmcnt(24)
	v_mul_f32_e32 v4, 0x43800000, v126
	v_med3_f32 v18, v18, s0, v1
	v_med3_f32 v4, v4, s0, v1
	v_cvt_pk_fp8_f32 v13, v18, v4 op_sel:[0,0,1]
	v_mul_f32_e32 v4, 0x43800000, v35
	v_mul_f32_e32 v18, 0x43800000, v39
	v_med3_f32 v4, v4, s0, v1
	v_med3_f32 v20, v18, s0, v1
	v_mov_b32_e32 v18, v5
	v_cvt_pk_fp8_f32 v18, v4, v20
	v_mul_f32_e32 v19, 0x43800000, v59
	v_mul_f32_e32 v4, 0x43800000, v51
	v_med3_f32 v19, v19, s0, v1
	v_med3_f32 v4, v4, s0, v1
	v_cvt_pk_fp8_f32 v18, v19, v4 op_sel:[0,0,1]
	v_mul_f32_e32 v4, 0x43800000, v67
	v_mul_f32_e32 v19, 0x43800000, v71
	v_med3_f32 v4, v4, s0, v1
	v_med3_f32 v21, v19, s0, v1
	v_mov_b32_e32 v19, v5
	v_cvt_pk_fp8_f32 v19, v4, v21
	v_mul_f32_e32 v20, 0x43800000, v95
	v_mul_f32_e32 v4, 0x43800000, v83
	v_med3_f32 v20, v20, s0, v1
	v_med3_f32 v4, v4, s0, v1
	v_cvt_pk_fp8_f32 v19, v20, v4 op_sel:[0,0,1]
	v_mul_f32_e32 v4, 0x43800000, v99
	v_mul_f32_e32 v20, 0x43800000, v103
	v_med3_f32 v4, v4, s0, v1
	v_med3_f32 v26, v20, s0, v1
	v_mov_b32_e32 v20, v5
	v_cvt_pk_fp8_f32 v20, v4, v26
	v_mul_f32_e32 v21, 0x43800000, v115
	v_mul_f32_e32 v4, 0x43800000, v111
	v_med3_f32 v21, v21, s0, v1
	v_med3_f32 v4, v4, s0, v1
	v_cvt_pk_fp8_f32 v20, v21, v4 op_sel:[0,0,1]
	v_mul_f32_e32 v4, 0x43800000, v119
	v_mul_f32_e32 v21, 0x43800000, v123
	v_med3_f32 v4, v4, s0, v1
	v_med3_f32 v27, v21, s0, v1
	v_mov_b32_e32 v21, v5
	v_cvt_pk_fp8_f32 v21, v4, v27
	v_mul_f32_e32 v26, 0x43800000, v131
	v_mul_f32_e32 v4, 0x43800000, v127
	v_med3_f32 v26, v26, s0, v1
	v_med3_f32 v4, v4, s0, v1
	v_cvt_pk_fp8_f32 v21, v26, v4 op_sel:[0,0,1]
	v_mul_f32_e32 v4, 0x43800000, v36
	v_mul_f32_e32 v26, 0x43800000, v40
	v_med3_f32 v4, v4, s0, v1
	v_med3_f32 v28, v26, s0, v1
	v_mov_b32_e32 v26, v5
	v_cvt_pk_fp8_f32 v26, v4, v28
	v_mul_f32_e32 v27, 0x43800000, v60
	v_mul_f32_e32 v4, 0x43800000, v52
	v_med3_f32 v27, v27, s0, v1
	v_med3_f32 v4, v4, s0, v1
	v_cvt_pk_fp8_f32 v26, v27, v4 op_sel:[0,0,1]
	v_mul_f32_e32 v4, 0x43800000, v68
	v_mul_f32_e32 v27, 0x43800000, v72
	v_med3_f32 v4, v4, s0, v1
	v_med3_f32 v29, v27, s0, v1
	v_mov_b32_e32 v27, v5
	v_cvt_pk_fp8_f32 v27, v4, v29
	v_mul_f32_e32 v28, 0x43800000, v96
	v_mul_f32_e32 v4, 0x43800000, v84
	v_med3_f32 v28, v28, s0, v1
	v_med3_f32 v4, v4, s0, v1
	v_cvt_pk_fp8_f32 v27, v28, v4 op_sel:[0,0,1]
	v_mul_f32_e32 v4, 0x43800000, v100
	v_mul_f32_e32 v28, 0x43800000, v104
	v_med3_f32 v4, v4, s0, v1
	v_med3_f32 v34, v28, s0, v1
	v_mov_b32_e32 v28, v5
	v_cvt_pk_fp8_f32 v28, v4, v34
	v_mul_f32_e32 v29, 0x43800000, v116
	v_mul_f32_e32 v4, 0x43800000, v112
	v_med3_f32 v29, v29, s0, v1
	v_med3_f32 v4, v4, s0, v1
	v_cvt_pk_fp8_f32 v28, v29, v4 op_sel:[0,0,1]
	v_mul_f32_e32 v4, 0x43800000, v120
	v_mul_f32_e32 v29, 0x43800000, v124
	v_med3_f32 v4, v4, s0, v1
	v_med3_f32 v35, v29, s0, v1
	v_mov_b32_e32 v29, v5
	v_cvt_pk_fp8_f32 v29, v4, v35
	v_mul_f32_e32 v34, 0x43800000, v132
	v_mul_f32_e32 v4, 0x43800000, v128
	v_med3_f32 v34, v34, s0, v1
	v_med3_f32 v4, v4, s0, v1
	v_cvt_pk_fp8_f32 v29, v34, v4 op_sel:[0,0,1]
	v_mul_f32_e32 v4, 0x43800000, v37
	v_mul_f32_e32 v34, 0x43800000, v41
	v_med3_f32 v4, v4, s0, v1
	v_med3_f32 v36, v34, s0, v1
	v_mov_b32_e32 v34, v5
	v_cvt_pk_fp8_f32 v34, v4, v36
	v_mul_f32_e32 v35, 0x43800000, v61
	v_mul_f32_e32 v4, 0x43800000, v53
	v_med3_f32 v35, v35, s0, v1
	v_med3_f32 v4, v4, s0, v1
	v_cvt_pk_fp8_f32 v34, v35, v4 op_sel:[0,0,1]
	v_mul_f32_e32 v4, 0x43800000, v69
	v_mul_f32_e32 v35, 0x43800000, v73
	v_med3_f32 v4, v4, s0, v1
	v_med3_f32 v37, v35, s0, v1
	v_mov_b32_e32 v35, v5
	v_cvt_pk_fp8_f32 v35, v4, v37
	v_mul_f32_e32 v36, 0x43800000, v97
	v_mul_f32_e32 v4, 0x43800000, v85
	v_med3_f32 v36, v36, s0, v1
	v_med3_f32 v4, v4, s0, v1
	v_cvt_pk_fp8_f32 v35, v36, v4 op_sel:[0,0,1]
	v_mul_f32_e32 v4, 0x43800000, v101
	v_mul_f32_e32 v36, 0x43800000, v105
	v_med3_f32 v4, v4, s0, v1
	v_med3_f32 v38, v36, s0, v1
	v_mov_b32_e32 v36, v5
	v_cvt_pk_fp8_f32 v36, v4, v38
	v_mul_f32_e32 v37, 0x43800000, v117
	v_mul_f32_e32 v4, 0x43800000, v113
	v_med3_f32 v37, v37, s0, v1
	v_med3_f32 v4, v4, s0, v1
	v_cvt_pk_fp8_f32 v36, v37, v4 op_sel:[0,0,1]
	v_mul_f32_e32 v4, 0x43800000, v121
	v_mul_f32_e32 v37, 0x43800000, v125
	v_med3_f32 v4, v4, s0, v1
	v_med3_f32 v39, v37, s0, v1
	v_mov_b32_e32 v37, v5
	v_cvt_pk_fp8_f32 v37, v4, v39
	v_mul_f32_e32 v38, 0x43800000, v133
	v_mul_f32_e32 v4, 0x43800000, v129
	v_med3_f32 v38, v38, s0, v1
	v_med3_f32 v4, v4, s0, v1
	v_cvt_pk_fp8_f32 v37, v38, v4 op_sel:[0,0,1]
	ds_write_b128 v166, v[10:13]
	ds_write_b128 v166, v[18:21] offset:272
	ds_write_b128 v166, v[26:29] offset:544
	ds_write_b128 v166, v[34:37] offset:816
	s_waitcnt lgkmcnt(0)
	s_barrier
	s_mov_b32 s1, 0x800000
	v_add_co_u32_e32 v10, vcc, s1, v2
	s_mov_b32 s1, 0x802000
	s_nop 0
	v_addc_co_u32_e32 v11, vcc, 0, v3, vcc
	v_add_co_u32_e32 v18, vcc, s1, v2
	s_mov_b32 s1, 0x804000
	s_nop 0
	v_addc_co_u32_e32 v19, vcc, 0, v3, vcc
	v_add_co_u32_e32 v38, vcc, s1, v2
	s_mov_b32 s1, 0x806000
	s_nop 0
	v_addc_co_u32_e32 v39, vcc, 0, v3, vcc
	v_add_co_u32_e32 v40, vcc, s1, v2
	s_mov_b32 s1, 0x808000
	s_nop 0
	v_addc_co_u32_e32 v41, vcc, 0, v3, vcc
	v_add_co_u32_e32 v58, vcc, s1, v2
	s_mov_b32 s1, 0x80a000
	s_nop 0
	v_addc_co_u32_e32 v59, vcc, 0, v3, vcc
	v_add_co_u32_e32 v60, vcc, s1, v2
	s_mov_b32 s1, 0x80c000
	s_nop 0
	v_addc_co_u32_e32 v61, vcc, 0, v3, vcc
	v_add_co_u32_e32 v70, vcc, s1, v2
	s_mov_b32 s1, 0x80e000
	s_nop 0
	v_addc_co_u32_e32 v71, vcc, 0, v3, vcc
	v_add_co_u32_e32 v72, vcc, s1, v2
	s_mov_b32 s1, 0x810000
	s_nop 0
	v_addc_co_u32_e32 v73, vcc, 0, v3, vcc
	v_add_co_u32_e32 v90, vcc, s1, v2
	s_mov_b32 s1, 0x812000
	s_nop 0
	v_addc_co_u32_e32 v91, vcc, 0, v3, vcc
	v_add_co_u32_e32 v92, vcc, s1, v2
	s_mov_b32 s1, 0x814000
	s_nop 0
	v_addc_co_u32_e32 v93, vcc, 0, v3, vcc
	global_load_dwordx4 v[10:13], v[10:11], off sc0 nt
	s_nop 0
	global_load_dwordx4 v[18:21], v[18:19], off sc0 nt
	s_nop 0
	global_load_dwordx4 v[34:37], v[38:39], off sc0 nt
	global_load_dwordx4 v[26:29], v[40:41], off sc0 nt
	s_nop 0
	global_load_dwordx4 v[38:41], v[58:59], off sc0 nt
	global_load_dwordx4 v[50:53], v[60:61], off sc0 nt
	global_load_dwordx4 v[66:69], v[70:71], off sc0 nt
	s_nop 0
	global_load_dwordx4 v[58:61], v[72:73], off sc0 nt
	s_nop 0
	global_load_dwordx4 v[70:73], v[90:91], off sc0 nt
	global_load_dwordx4 v[82:85], v[92:93], off sc0 nt
	v_add_co_u32_e32 v90, vcc, s1, v2
	s_mov_b32 s1, 0x816000
	s_nop 0
	v_addc_co_u32_e32 v91, vcc, 0, v3, vcc
	v_add_co_u32_e32 v92, vcc, s1, v2
	s_mov_b32 s1, 0x818000
	s_nop 0
	v_addc_co_u32_e32 v93, vcc, 0, v3, vcc
	v_add_co_u32_e32 v98, vcc, s1, v2
	s_mov_b32 s1, 0x81a000
	s_nop 0
	v_addc_co_u32_e32 v99, vcc, 0, v3, vcc
	v_add_co_u32_e32 v102, vcc, s1, v2
	s_mov_b32 s1, 0x81c000
	s_nop 0
	v_addc_co_u32_e32 v103, vcc, 0, v3, vcc
	global_load_dwordx4 v[94:97], v[90:91], off sc0 nt
	s_nop 0
	global_load_dwordx4 v[90:93], v[92:93], off sc0 nt
	s_nop 0
	global_load_dwordx4 v[98:101], v[98:99], off sc0 nt
	s_nop 0
	global_load_dwordx4 v[110:113], v[102:103], off sc0 nt
	v_add_co_u32_e32 v102, vcc, s1, v2
	s_mov_b32 s1, 0x81e000
	s_nop 0
	v_addc_co_u32_e32 v103, vcc, 0, v3, vcc
	v_add_co_u32_e32 v104, vcc, s1, v2
	s_nop 1
	v_addc_co_u32_e32 v105, vcc, 0, v3, vcc
	global_load_dwordx4 v[126:129], v[102:103], off sc0 nt
	global_load_dwordx4 v[118:121], v[104:105], off sc0 nt
	ds_read_b128 v[102:105], v154
	ds_read_b128 v[114:117], v156
	ds_read_b128 v[122:125], v158
	ds_read_b128 v[130:133], v162
	s_waitcnt lgkmcnt(3)
	global_store_dwordx4 v[150:151], v[102:105], off offset:512 nt
	s_waitcnt lgkmcnt(2)
	global_store_dwordx4 v[152:153], v[114:117], off offset:512 nt
	s_waitcnt lgkmcnt(1)
	global_store_dwordx4 v[160:161], v[122:125], off offset:512 nt
	s_waitcnt lgkmcnt(0)
	global_store_dwordx4 v[164:165], v[130:133], off offset:512 nt
	s_waitcnt vmcnt(39)
	v_mul_f32_e32 v4, 0x43800000, v6
	s_waitcnt vmcnt(38)
	v_mul_f32_e32 v6, 0x43800000, v14
	v_med3_f32 v4, v4, s0, v1
	v_med3_f32 v6, v6, s0, v1
	v_mov_b32_e32 v102, v5
	v_cvt_pk_fp8_f32 v102, v4, v6
	s_waitcnt vmcnt(37)
	v_mul_f32_e32 v14, 0x43800000, v30
	s_waitcnt vmcnt(36)
	v_mul_f32_e32 v4, 0x43800000, v22
	v_med3_f32 v6, v14, s0, v1
	v_med3_f32 v4, v4, s0, v1
	v_cvt_pk_fp8_f32 v102, v6, v4 op_sel:[0,0,1]
	s_waitcnt vmcnt(35)
	v_mul_f32_e32 v4, 0x43800000, v42
	s_waitcnt vmcnt(34)
	v_mul_f32_e32 v6, 0x43800000, v46
	v_med3_f32 v4, v4, s0, v1
	v_med3_f32 v6, v6, s0, v1
	v_mov_b32_e32 v103, v5
	v_cvt_pk_fp8_f32 v103, v4, v6
	s_waitcnt vmcnt(33)
	v_mul_f32_e32 v14, 0x43800000, v62
	s_waitcnt vmcnt(32)
	v_mul_f32_e32 v4, 0x43800000, v54
	v_med3_f32 v6, v14, s0, v1
	v_med3_f32 v4, v4, s0, v1
	v_cvt_pk_fp8_f32 v103, v6, v4 op_sel:[0,0,1]
	s_waitcnt vmcnt(31)
	v_mul_f32_e32 v4, 0x43800000, v74
	s_waitcnt vmcnt(30)
	v_mul_f32_e32 v6, 0x43800000, v78
	v_med3_f32 v4, v4, s0, v1
	v_med3_f32 v6, v6, s0, v1
	v_mov_b32_e32 v104, v5
	v_cvt_pk_fp8_f32 v104, v4, v6
	s_waitcnt vmcnt(29)
	v_mul_f32_e32 v14, 0x43800000, v106
	s_waitcnt vmcnt(28)
	v_mul_f32_e32 v4, 0x43800000, v86
	v_med3_f32 v6, v14, s0, v1
	v_med3_f32 v4, v4, s0, v1
	v_cvt_pk_fp8_f32 v104, v6, v4 op_sel:[0,0,1]
	s_waitcnt vmcnt(27)
	v_mul_f32_e32 v4, 0x43800000, v134
	s_waitcnt vmcnt(26)
	v_mul_f32_e32 v6, 0x43800000, v138
	v_med3_f32 v4, v4, s0, v1
	v_med3_f32 v6, v6, s0, v1
	v_mov_b32_e32 v105, v5
	v_cvt_pk_fp8_f32 v105, v4, v6
	s_waitcnt vmcnt(25)
	v_mul_f32_e32 v14, 0x43800000, v146
	s_waitcnt vmcnt(24)
	v_mul_f32_e32 v4, 0x43800000, v142
	v_med3_f32 v6, v14, s0, v1
	v_med3_f32 v4, v4, s0, v1
	v_cvt_pk_fp8_f32 v105, v6, v4 op_sel:[0,0,1]
	v_mul_f32_e32 v4, 0x43800000, v7
	v_mul_f32_e32 v6, 0x43800000, v15
	v_med3_f32 v4, v4, s0, v1
	v_med3_f32 v6, v6, s0, v1
	v_mov_b32_e32 v114, v5
	v_cvt_pk_fp8_f32 v114, v4, v6
	v_mul_f32_e32 v7, 0x43800000, v31
	v_mul_f32_e32 v4, 0x43800000, v23
	v_med3_f32 v6, v7, s0, v1
	v_med3_f32 v4, v4, s0, v1
	v_cvt_pk_fp8_f32 v114, v6, v4 op_sel:[0,0,1]
	v_mul_f32_e32 v4, 0x43800000, v43
	v_mul_f32_e32 v6, 0x43800000, v47
	v_med3_f32 v4, v4, s0, v1
	v_med3_f32 v6, v6, s0, v1
	v_mov_b32_e32 v115, v5
	v_cvt_pk_fp8_f32 v115, v4, v6
	v_mul_f32_e32 v7, 0x43800000, v63
	v_mul_f32_e32 v4, 0x43800000, v55
	v_med3_f32 v6, v7, s0, v1
	v_med3_f32 v4, v4, s0, v1
	v_cvt_pk_fp8_f32 v115, v6, v4 op_sel:[0,0,1]
	v_mul_f32_e32 v4, 0x43800000, v75
	v_mul_f32_e32 v6, 0x43800000, v79
	v_med3_f32 v4, v4, s0, v1
	v_med3_f32 v6, v6, s0, v1
	v_mov_b32_e32 v116, v5
	v_cvt_pk_fp8_f32 v116, v4, v6
	v_mul_f32_e32 v7, 0x43800000, v107
	v_mul_f32_e32 v4, 0x43800000, v87
	v_med3_f32 v6, v7, s0, v1
	v_med3_f32 v4, v4, s0, v1
	v_cvt_pk_fp8_f32 v116, v6, v4 op_sel:[0,0,1]
	v_mul_f32_e32 v4, 0x43800000, v135
	v_mul_f32_e32 v6, 0x43800000, v139
	v_med3_f32 v4, v4, s0, v1
	v_med3_f32 v6, v6, s0, v1
	v_mov_b32_e32 v117, v5
	v_cvt_pk_fp8_f32 v117, v4, v6
	v_mul_f32_e32 v7, 0x43800000, v147
	v_mul_f32_e32 v4, 0x43800000, v143
	v_med3_f32 v6, v7, s0, v1
	v_med3_f32 v4, v4, s0, v1
	v_cvt_pk_fp8_f32 v117, v6, v4 op_sel:[0,0,1]
	v_mul_f32_e32 v4, 0x43800000, v8
	v_mul_f32_e32 v6, 0x43800000, v16
	v_med3_f32 v4, v4, s0, v1
	v_med3_f32 v6, v6, s0, v1
	v_mov_b32_e32 v122, v5
	v_cvt_pk_fp8_f32 v122, v4, v6
	v_mul_f32_e32 v7, 0x43800000, v32
	v_mul_f32_e32 v4, 0x43800000, v24
	v_med3_f32 v6, v7, s0, v1
	v_med3_f32 v4, v4, s0, v1
	v_cvt_pk_fp8_f32 v122, v6, v4 op_sel:[0,0,1]
	v_mul_f32_e32 v4, 0x43800000, v44
	v_mul_f32_e32 v6, 0x43800000, v48
	v_med3_f32 v4, v4, s0, v1
	v_med3_f32 v6, v6, s0, v1
	v_mov_b32_e32 v123, v5
	v_cvt_pk_fp8_f32 v123, v4, v6
	v_mul_f32_e32 v7, 0x43800000, v64
	v_mul_f32_e32 v4, 0x43800000, v56
	v_med3_f32 v6, v7, s0, v1
	v_med3_f32 v4, v4, s0, v1
	v_cvt_pk_fp8_f32 v123, v6, v4 op_sel:[0,0,1]
	v_mul_f32_e32 v4, 0x43800000, v76
	v_mul_f32_e32 v6, 0x43800000, v80
	v_med3_f32 v4, v4, s0, v1
	v_med3_f32 v6, v6, s0, v1
	v_mov_b32_e32 v124, v5
	v_cvt_pk_fp8_f32 v124, v4, v6
	v_mul_f32_e32 v7, 0x43800000, v108
	v_mul_f32_e32 v4, 0x43800000, v88
	v_med3_f32 v6, v7, s0, v1
	v_med3_f32 v4, v4, s0, v1
	v_cvt_pk_fp8_f32 v124, v6, v4 op_sel:[0,0,1]
	v_mul_f32_e32 v4, 0x43800000, v136
	v_mul_f32_e32 v6, 0x43800000, v140
	v_med3_f32 v4, v4, s0, v1
	v_med3_f32 v6, v6, s0, v1
	v_mov_b32_e32 v125, v5
	v_cvt_pk_fp8_f32 v125, v4, v6
	v_mul_f32_e32 v7, 0x43800000, v148
	v_mul_f32_e32 v4, 0x43800000, v144
	v_med3_f32 v6, v7, s0, v1
	v_med3_f32 v4, v4, s0, v1
	v_cvt_pk_fp8_f32 v125, v6, v4 op_sel:[0,0,1]
	v_mul_f32_e32 v4, 0x43800000, v9
	v_mul_f32_e32 v6, 0x43800000, v17
	v_med3_f32 v4, v4, s0, v1
	v_med3_f32 v8, v6, s0, v1
	v_mov_b32_e32 v6, v5
	v_cvt_pk_fp8_f32 v6, v4, v8
	v_mul_f32_e32 v7, 0x43800000, v33
	v_mul_f32_e32 v4, 0x43800000, v25
	v_med3_f32 v7, v7, s0, v1
	v_med3_f32 v4, v4, s0, v1
	v_cvt_pk_fp8_f32 v6, v7, v4 op_sel:[0,0,1]
	v_mul_f32_e32 v4, 0x43800000, v45
	v_mul_f32_e32 v7, 0x43800000, v49
	v_med3_f32 v4, v4, s0, v1
	v_med3_f32 v9, v7, s0, v1
	v_mov_b32_e32 v7, v5
	v_cvt_pk_fp8_f32 v7, v4, v9
	v_mul_f32_e32 v8, 0x43800000, v65
	v_mul_f32_e32 v4, 0x43800000, v57
	v_med3_f32 v8, v8, s0, v1
	v_med3_f32 v4, v4, s0, v1
	v_cvt_pk_fp8_f32 v7, v8, v4 op_sel:[0,0,1]
	v_mul_f32_e32 v4, 0x43800000, v77
	v_mul_f32_e32 v8, 0x43800000, v81
	v_med3_f32 v4, v4, s0, v1
	v_med3_f32 v14, v8, s0, v1
	v_mov_b32_e32 v8, v5
	v_cvt_pk_fp8_f32 v8, v4, v14
	v_mul_f32_e32 v9, 0x43800000, v109
	v_mul_f32_e32 v4, 0x43800000, v89
	v_med3_f32 v9, v9, s0, v1
	v_med3_f32 v4, v4, s0, v1
	v_cvt_pk_fp8_f32 v8, v9, v4 op_sel:[0,0,1]
	v_mul_f32_e32 v4, 0x43800000, v137
	v_mul_f32_e32 v9, 0x43800000, v141
	v_med3_f32 v4, v4, s0, v1
	v_med3_f32 v15, v9, s0, v1
	v_mov_b32_e32 v9, v5
	v_cvt_pk_fp8_f32 v9, v4, v15
	v_mul_f32_e32 v14, 0x43800000, v149
	v_mul_f32_e32 v4, 0x43800000, v145
	v_med3_f32 v14, v14, s0, v1
	v_med3_f32 v4, v4, s0, v1
	v_cvt_pk_fp8_f32 v9, v14, v4 op_sel:[0,0,1]
	ds_write_b128 v166, v[102:105] offset:34816
	ds_write_b128 v166, v[114:117] offset:35088
	ds_write_b128 v166, v[122:125] offset:35360
	ds_write_b128 v166, v[6:9] offset:35632
	s_waitcnt lgkmcnt(0)
	s_barrier
	s_mov_b32 s1, 0xa00000
	v_add_co_u32_e32 v6, vcc, s1, v2
	s_mov_b32 s1, 0xa02000
	s_nop 0
	v_addc_co_u32_e32 v7, vcc, 0, v3, vcc
	v_add_co_u32_e32 v14, vcc, s1, v2
	s_mov_b32 s1, 0xa04000
	s_nop 0
	v_addc_co_u32_e32 v15, vcc, 0, v3, vcc
	v_add_co_u32_e32 v42, vcc, s1, v2
	s_mov_b32 s1, 0xa06000
	s_nop 0
	v_addc_co_u32_e32 v43, vcc, 0, v3, vcc
	v_add_co_u32_e32 v44, vcc, s1, v2
	s_mov_b32 s1, 0xa08000
	s_nop 0
	v_addc_co_u32_e32 v45, vcc, 0, v3, vcc
	v_add_co_u32_e32 v54, vcc, s1, v2
	s_mov_b32 s1, 0xa0a000
	s_nop 0
	v_addc_co_u32_e32 v55, vcc, 0, v3, vcc
	v_add_co_u32_e32 v56, vcc, s1, v2
	s_mov_b32 s1, 0xa0c000
	s_nop 0
	v_addc_co_u32_e32 v57, vcc, 0, v3, vcc
	v_add_co_u32_e32 v74, vcc, s1, v2
	s_mov_b32 s1, 0xa0e000
	s_nop 0
	v_addc_co_u32_e32 v75, vcc, 0, v3, vcc
	v_add_co_u32_e32 v76, vcc, s1, v2
	s_mov_b32 s1, 0xa10000
	s_nop 0
	v_addc_co_u32_e32 v77, vcc, 0, v3, vcc
	v_add_co_u32_e32 v86, vcc, s1, v2
	s_mov_b32 s1, 0xa12000
	s_nop 0
	v_addc_co_u32_e32 v87, vcc, 0, v3, vcc
	v_add_co_u32_e32 v88, vcc, s1, v2
	s_mov_b32 s1, 0xa14000
	s_nop 0
	v_addc_co_u32_e32 v89, vcc, 0, v3, vcc
	global_load_dwordx4 v[6:9], v[6:7], off sc0 nt
	s_nop 0
	global_load_dwordx4 v[14:17], v[14:15], off sc0 nt
	s_nop 0
	global_load_dwordx4 v[30:33], v[42:43], off sc0 nt
	global_load_dwordx4 v[22:25], v[44:45], off sc0 nt
	s_nop 0
	global_load_dwordx4 v[42:45], v[54:55], off sc0 nt
	global_load_dwordx4 v[46:49], v[56:57], off sc0 nt
	global_load_dwordx4 v[62:65], v[74:75], off sc0 nt
	s_nop 0
	global_load_dwordx4 v[54:57], v[76:77], off sc0 nt
	s_nop 0
	global_load_dwordx4 v[74:77], v[86:87], off sc0 nt
	global_load_dwordx4 v[78:81], v[88:89], off sc0 nt
	v_add_co_u32_e32 v86, vcc, s1, v2
	s_mov_b32 s1, 0xa16000
	s_nop 0
	v_addc_co_u32_e32 v87, vcc, 0, v3, vcc
	v_add_co_u32_e32 v88, vcc, s1, v2
	s_mov_b32 s1, 0xa18000
	s_nop 0
	v_addc_co_u32_e32 v89, vcc, 0, v3, vcc
	v_add_co_u32_e32 v106, vcc, s1, v2
	s_mov_b32 s1, 0xa1a000
	s_nop 0
	v_addc_co_u32_e32 v107, vcc, 0, v3, vcc
	v_add_co_u32_e32 v114, vcc, s1, v2
	s_mov_b32 s1, 0xa1c000
	s_nop 0
	v_addc_co_u32_e32 v115, vcc, 0, v3, vcc
	v_add_co_u32_e32 v122, vcc, s1, v2
	s_mov_b32 s1, 0xa1e000
	s_nop 0
	v_addc_co_u32_e32 v123, vcc, 0, v3, vcc
	v_add_co_u32_e32 v124, vcc, s1, v2
	global_load_dwordx4 v[102:105], v[86:87], off sc0 nt
	s_nop 0
	global_load_dwordx4 v[86:89], v[88:89], off sc0 nt
	v_addc_co_u32_e32 v125, vcc, 0, v3, vcc
	global_load_dwordx4 v[106:109], v[106:107], off sc0 nt
	s_nop 0
	global_load_dwordx4 v[114:117], v[114:115], off sc0 nt
	s_nop 0
	global_load_dwordx4 v[130:133], v[122:123], off sc0 nt
	s_nop 0
	global_load_dwordx4 v[122:125], v[124:125], off sc0 nt
	ds_read_b128 v[134:137], v154 offset:34816
	ds_read_b128 v[138:141], v156 offset:34816
	ds_read_b128 v[142:145], v158 offset:34816
	ds_read_b128 v[146:149], v162 offset:34816
	s_waitcnt lgkmcnt(3)
	global_store_dwordx4 v[150:151], v[134:137], off offset:768 nt
	s_waitcnt lgkmcnt(2)
	global_store_dwordx4 v[152:153], v[138:141], off offset:768 nt
	s_waitcnt lgkmcnt(1)
	global_store_dwordx4 v[160:161], v[142:145], off offset:768 nt
	s_waitcnt lgkmcnt(0)
	global_store_dwordx4 v[164:165], v[146:149], off offset:768 nt
	s_waitcnt vmcnt(39)
	v_mul_f32_e32 v4, 0x43800000, v10
	s_waitcnt vmcnt(38)
	v_mul_f32_e32 v10, 0x43800000, v18
	v_med3_f32 v4, v4, s0, v1
	v_med3_f32 v10, v10, s0, v1
	v_mov_b32_e32 v134, v5
	v_cvt_pk_fp8_f32 v134, v4, v10
	s_waitcnt vmcnt(37)
	v_mul_f32_e32 v18, 0x43800000, v34
	s_waitcnt vmcnt(36)
	v_mul_f32_e32 v4, 0x43800000, v26
	v_med3_f32 v10, v18, s0, v1
	v_med3_f32 v4, v4, s0, v1
	v_cvt_pk_fp8_f32 v134, v10, v4 op_sel:[0,0,1]
	s_waitcnt vmcnt(35)
	v_mul_f32_e32 v4, 0x43800000, v38
	s_waitcnt vmcnt(34)
	v_mul_f32_e32 v10, 0x43800000, v50
	v_med3_f32 v4, v4, s0, v1
	v_med3_f32 v10, v10, s0, v1
	v_mov_b32_e32 v135, v5
	v_cvt_pk_fp8_f32 v135, v4, v10
	s_waitcnt vmcnt(33)
	v_mul_f32_e32 v18, 0x43800000, v66
	s_waitcnt vmcnt(32)
	v_mul_f32_e32 v4, 0x43800000, v58
	v_med3_f32 v10, v18, s0, v1
	v_med3_f32 v4, v4, s0, v1
	v_cvt_pk_fp8_f32 v135, v10, v4 op_sel:[0,0,1]
	s_waitcnt vmcnt(31)
	v_mul_f32_e32 v4, 0x43800000, v70
	s_waitcnt vmcnt(30)
	v_mul_f32_e32 v10, 0x43800000, v82
	v_med3_f32 v4, v4, s0, v1
	v_med3_f32 v10, v10, s0, v1
	v_mov_b32_e32 v136, v5
	v_cvt_pk_fp8_f32 v136, v4, v10
	s_waitcnt vmcnt(29)
	v_mul_f32_e32 v18, 0x43800000, v94
	s_waitcnt vmcnt(28)
	v_mul_f32_e32 v4, 0x43800000, v90
	v_med3_f32 v10, v18, s0, v1
	v_med3_f32 v4, v4, s0, v1
	v_cvt_pk_fp8_f32 v136, v10, v4 op_sel:[0,0,1]
	s_waitcnt vmcnt(27)
	v_mul_f32_e32 v4, 0x43800000, v98
	s_waitcnt vmcnt(26)
	v_mul_f32_e32 v10, 0x43800000, v110
	v_med3_f32 v4, v4, s0, v1
	v_med3_f32 v10, v10, s0, v1
	v_mov_b32_e32 v137, v5
	v_cvt_pk_fp8_f32 v137, v4, v10
	s_waitcnt vmcnt(25)
	v_mul_f32_e32 v18, 0x43800000, v126
	s_waitcnt vmcnt(24)
	v_mul_f32_e32 v4, 0x43800000, v118
	v_med3_f32 v10, v18, s0, v1
	v_med3_f32 v4, v4, s0, v1
	v_cvt_pk_fp8_f32 v137, v10, v4 op_sel:[0,0,1]
	v_mul_f32_e32 v4, 0x43800000, v11
	v_mul_f32_e32 v10, 0x43800000, v19
	v_med3_f32 v4, v4, s0, v1
	v_med3_f32 v10, v10, s0, v1
	v_mov_b32_e32 v138, v5
	v_cvt_pk_fp8_f32 v138, v4, v10
	v_mul_f32_e32 v11, 0x43800000, v35
	v_mul_f32_e32 v4, 0x43800000, v27
	v_med3_f32 v10, v11, s0, v1
	v_med3_f32 v4, v4, s0, v1
	v_cvt_pk_fp8_f32 v138, v10, v4 op_sel:[0,0,1]
	v_mul_f32_e32 v4, 0x43800000, v39
	v_mul_f32_e32 v10, 0x43800000, v51
	v_med3_f32 v4, v4, s0, v1
	v_med3_f32 v10, v10, s0, v1
	v_mov_b32_e32 v139, v5
	v_cvt_pk_fp8_f32 v139, v4, v10
	v_mul_f32_e32 v11, 0x43800000, v67
	v_mul_f32_e32 v4, 0x43800000, v59
	v_med3_f32 v10, v11, s0, v1
	v_med3_f32 v4, v4, s0, v1
	v_cvt_pk_fp8_f32 v139, v10, v4 op_sel:[0,0,1]
	v_mul_f32_e32 v4, 0x43800000, v71
	v_mul_f32_e32 v10, 0x43800000, v83
	v_med3_f32 v4, v4, s0, v1
	v_med3_f32 v10, v10, s0, v1
	v_mov_b32_e32 v140, v5
	v_cvt_pk_fp8_f32 v140, v4, v10
	v_mul_f32_e32 v11, 0x43800000, v95
	v_mul_f32_e32 v4, 0x43800000, v91
	v_med3_f32 v10, v11, s0, v1
	v_med3_f32 v4, v4, s0, v1
	v_cvt_pk_fp8_f32 v140, v10, v4 op_sel:[0,0,1]
	v_mul_f32_e32 v4, 0x43800000, v99
	v_mul_f32_e32 v10, 0x43800000, v111
	v_med3_f32 v4, v4, s0, v1
	v_med3_f32 v10, v10, s0, v1
	v_mov_b32_e32 v141, v5
	v_cvt_pk_fp8_f32 v141, v4, v10
	v_mul_f32_e32 v11, 0x43800000, v127
	v_mul_f32_e32 v4, 0x43800000, v119
	v_med3_f32 v10, v11, s0, v1
	v_med3_f32 v4, v4, s0, v1
	v_cvt_pk_fp8_f32 v141, v10, v4 op_sel:[0,0,1]
	v_mul_f32_e32 v4, 0x43800000, v12
	v_mul_f32_e32 v10, 0x43800000, v20
	v_med3_f32 v4, v4, s0, v1
	v_med3_f32 v10, v10, s0, v1
	v_mov_b32_e32 v142, v5
	v_cvt_pk_fp8_f32 v142, v4, v10
	v_mul_f32_e32 v11, 0x43800000, v36
	v_mul_f32_e32 v4, 0x43800000, v28
	v_med3_f32 v10, v11, s0, v1
	v_med3_f32 v4, v4, s0, v1
	v_cvt_pk_fp8_f32 v142, v10, v4 op_sel:[0,0,1]
	v_mul_f32_e32 v4, 0x43800000, v40
	v_mul_f32_e32 v10, 0x43800000, v52
	v_med3_f32 v4, v4, s0, v1
	v_med3_f32 v10, v10, s0, v1
	v_mov_b32_e32 v143, v5
	v_cvt_pk_fp8_f32 v143, v4, v10
	v_mul_f32_e32 v11, 0x43800000, v68
	v_mul_f32_e32 v4, 0x43800000, v60
	v_med3_f32 v10, v11, s0, v1
	v_med3_f32 v4, v4, s0, v1
	v_cvt_pk_fp8_f32 v143, v10, v4 op_sel:[0,0,1]
	v_mul_f32_e32 v4, 0x43800000, v72
	v_mul_f32_e32 v10, 0x43800000, v84
	v_med3_f32 v4, v4, s0, v1
	v_med3_f32 v10, v10, s0, v1
	v_mov_b32_e32 v144, v5
	v_cvt_pk_fp8_f32 v144, v4, v10
	v_mul_f32_e32 v11, 0x43800000, v96
	v_mul_f32_e32 v4, 0x43800000, v92
	v_med3_f32 v10, v11, s0, v1
	v_med3_f32 v4, v4, s0, v1
	v_cvt_pk_fp8_f32 v144, v10, v4 op_sel:[0,0,1]
	v_mul_f32_e32 v4, 0x43800000, v100
	v_mul_f32_e32 v10, 0x43800000, v112
	v_med3_f32 v4, v4, s0, v1
	v_med3_f32 v10, v10, s0, v1
	v_mov_b32_e32 v145, v5
	v_cvt_pk_fp8_f32 v145, v4, v10
	v_mul_f32_e32 v11, 0x43800000, v128
	v_mul_f32_e32 v4, 0x43800000, v120
	v_med3_f32 v10, v11, s0, v1
	v_med3_f32 v4, v4, s0, v1
	v_cvt_pk_fp8_f32 v145, v10, v4 op_sel:[0,0,1]
	v_mul_f32_e32 v4, 0x43800000, v13
	v_mul_f32_e32 v10, 0x43800000, v21
	v_med3_f32 v4, v4, s0, v1
	v_med3_f32 v12, v10, s0, v1
	v_mov_b32_e32 v10, v5
	v_cvt_pk_fp8_f32 v10, v4, v12
	v_mul_f32_e32 v11, 0x43800000, v37
	v_mul_f32_e32 v4, 0x43800000, v29
	v_med3_f32 v11, v11, s0, v1
	v_med3_f32 v4, v4, s0, v1
	v_cvt_pk_fp8_f32 v10, v11, v4 op_sel:[0,0,1]
	v_mul_f32_e32 v4, 0x43800000, v41
	v_mul_f32_e32 v11, 0x43800000, v53
	v_med3_f32 v4, v4, s0, v1
	v_med3_f32 v13, v11, s0, v1
	v_mov_b32_e32 v11, v5
	v_cvt_pk_fp8_f32 v11, v4, v13
	v_mul_f32_e32 v12, 0x43800000, v69
	v_mul_f32_e32 v4, 0x43800000, v61
	v_med3_f32 v12, v12, s0, v1
	v_med3_f32 v4, v4, s0, v1
	v_cvt_pk_fp8_f32 v11, v12, v4 op_sel:[0,0,1]
	v_mul_f32_e32 v4, 0x43800000, v73
	v_mul_f32_e32 v12, 0x43800000, v85
	v_med3_f32 v4, v4, s0, v1
	v_med3_f32 v18, v12, s0, v1
	v_mov_b32_e32 v12, v5
	v_cvt_pk_fp8_f32 v12, v4, v18
	v_mul_f32_e32 v13, 0x43800000, v97
	v_mul_f32_e32 v4, 0x43800000, v93
	v_med3_f32 v13, v13, s0, v1
	v_med3_f32 v4, v4, s0, v1
	v_cvt_pk_fp8_f32 v12, v13, v4 op_sel:[0,0,1]
	v_mul_f32_e32 v4, 0x43800000, v101
	v_mul_f32_e32 v13, 0x43800000, v113
	v_med3_f32 v4, v4, s0, v1
	v_med3_f32 v19, v13, s0, v1
	v_mov_b32_e32 v13, v5
	v_cvt_pk_fp8_f32 v13, v4, v19
	v_mul_f32_e32 v18, 0x43800000, v129
	v_mul_f32_e32 v4, 0x43800000, v121
	v_med3_f32 v18, v18, s0, v1
	v_med3_f32 v4, v4, s0, v1
	v_cvt_pk_fp8_f32 v13, v18, v4 op_sel:[0,0,1]
	ds_write_b128 v166, v[134:137]
	ds_write_b128 v166, v[138:141] offset:272
	ds_write_b128 v166, v[142:145] offset:544
	ds_write_b128 v166, v[10:13] offset:816
	s_waitcnt lgkmcnt(0)
	s_barrier
	s_mov_b32 s1, 0xc00000
	v_add_co_u32_e32 v10, vcc, s1, v2
	s_mov_b32 s1, 0xc02000
	s_nop 0
	v_addc_co_u32_e32 v11, vcc, 0, v3, vcc
	v_add_co_u32_e32 v18, vcc, s1, v2
	s_mov_b32 s1, 0xc04000
	s_nop 0
	v_addc_co_u32_e32 v19, vcc, 0, v3, vcc
	v_add_co_u32_e32 v38, vcc, s1, v2
	s_mov_b32 s1, 0xc06000
	s_nop 0
	v_addc_co_u32_e32 v39, vcc, 0, v3, vcc
	v_add_co_u32_e32 v40, vcc, s1, v2
	s_mov_b32 s1, 0xc08000
	s_nop 0
	v_addc_co_u32_e32 v41, vcc, 0, v3, vcc
	v_add_co_u32_e32 v58, vcc, s1, v2
	s_mov_b32 s1, 0xc0a000
	s_nop 0
	v_addc_co_u32_e32 v59, vcc, 0, v3, vcc
	v_add_co_u32_e32 v60, vcc, s1, v2
	s_mov_b32 s1, 0xc0c000
	s_nop 0
	v_addc_co_u32_e32 v61, vcc, 0, v3, vcc
	v_add_co_u32_e32 v70, vcc, s1, v2
	s_mov_b32 s1, 0xc0e000
	s_nop 0
	v_addc_co_u32_e32 v71, vcc, 0, v3, vcc
	v_add_co_u32_e32 v72, vcc, s1, v2
	s_mov_b32 s1, 0xc10000
	s_nop 0
	v_addc_co_u32_e32 v73, vcc, 0, v3, vcc
	v_add_co_u32_e32 v90, vcc, s1, v2
	s_mov_b32 s1, 0xc12000
	s_nop 0
	v_addc_co_u32_e32 v91, vcc, 0, v3, vcc
	v_add_co_u32_e32 v92, vcc, s1, v2
	s_mov_b32 s1, 0xc14000
	s_nop 0
	v_addc_co_u32_e32 v93, vcc, 0, v3, vcc
	global_load_dwordx4 v[10:13], v[10:11], off sc0 nt
	s_nop 0
	global_load_dwordx4 v[18:21], v[18:19], off sc0 nt
	s_nop 0
	global_load_dwordx4 v[34:37], v[38:39], off sc0 nt
	global_load_dwordx4 v[26:29], v[40:41], off sc0 nt
	s_nop 0
	global_load_dwordx4 v[38:41], v[58:59], off sc0 nt
	global_load_dwordx4 v[50:53], v[60:61], off sc0 nt
	global_load_dwordx4 v[66:69], v[70:71], off sc0 nt
	s_nop 0
	global_load_dwordx4 v[58:61], v[72:73], off sc0 nt
	s_nop 0
	global_load_dwordx4 v[70:73], v[90:91], off sc0 nt
	global_load_dwordx4 v[82:85], v[92:93], off sc0 nt
	v_add_co_u32_e32 v90, vcc, s1, v2
	s_mov_b32 s1, 0xc16000
	s_nop 0
	v_addc_co_u32_e32 v91, vcc, 0, v3, vcc
	v_add_co_u32_e32 v92, vcc, s1, v2
	s_mov_b32 s1, 0xc18000
	s_nop 0
	v_addc_co_u32_e32 v93, vcc, 0, v3, vcc
	v_add_co_u32_e32 v98, vcc, s1, v2
	s_mov_b32 s1, 0xc1a000
	s_nop 0
	v_addc_co_u32_e32 v99, vcc, 0, v3, vcc
	v_add_co_u32_e32 v110, vcc, s1, v2
	s_mov_b32 s1, 0xc1c000
	s_nop 0
	v_addc_co_u32_e32 v111, vcc, 0, v3, vcc
	v_add_co_u32_e32 v118, vcc, s1, v2
	s_mov_b32 s1, 0xc1e000
	s_nop 0
	v_addc_co_u32_e32 v119, vcc, 0, v3, vcc
	v_add_co_u32_e32 v120, vcc, s1, v2
	global_load_dwordx4 v[94:97], v[90:91], off sc0 nt
	s_nop 0
	global_load_dwordx4 v[90:93], v[92:93], off sc0 nt
	v_addc_co_u32_e32 v121, vcc, 0, v3, vcc
	global_load_dwordx4 v[98:101], v[98:99], off sc0 nt
	s_nop 0
	global_load_dwordx4 v[110:113], v[110:111], off sc0 nt
	s_nop 0
	global_load_dwordx4 v[126:129], v[118:119], off sc0 nt
	s_nop 0
	global_load_dwordx4 v[118:121], v[120:121], off sc0 nt
	ds_read_b128 v[134:137], v154
	ds_read_b128 v[138:141], v156
	ds_read_b128 v[142:145], v158
	ds_read_b128 v[146:149], v162
	s_waitcnt lgkmcnt(3)
	global_store_dwordx4 v[150:151], v[134:137], off offset:1024 nt
	s_waitcnt lgkmcnt(2)
	global_store_dwordx4 v[152:153], v[138:141], off offset:1024 nt
	s_waitcnt lgkmcnt(1)
	global_store_dwordx4 v[160:161], v[142:145], off offset:1024 nt
	s_waitcnt lgkmcnt(0)
	global_store_dwordx4 v[164:165], v[146:149], off offset:1024 nt
	s_waitcnt vmcnt(39)
	v_mul_f32_e32 v4, 0x43800000, v6
	s_waitcnt vmcnt(38)
	v_mul_f32_e32 v6, 0x43800000, v14
	v_med3_f32 v4, v4, s0, v1
	v_med3_f32 v6, v6, s0, v1
	v_mov_b32_e32 v134, v5
	v_cvt_pk_fp8_f32 v134, v4, v6
	s_waitcnt vmcnt(37)
	v_mul_f32_e32 v14, 0x43800000, v30
	s_waitcnt vmcnt(36)
	v_mul_f32_e32 v4, 0x43800000, v22
	v_med3_f32 v6, v14, s0, v1
	v_med3_f32 v4, v4, s0, v1
	v_cvt_pk_fp8_f32 v134, v6, v4 op_sel:[0,0,1]
	s_waitcnt vmcnt(35)
	v_mul_f32_e32 v4, 0x43800000, v42
	s_waitcnt vmcnt(34)
	v_mul_f32_e32 v6, 0x43800000, v46
	v_med3_f32 v4, v4, s0, v1
	v_med3_f32 v6, v6, s0, v1
	v_mov_b32_e32 v135, v5
	v_cvt_pk_fp8_f32 v135, v4, v6
	s_waitcnt vmcnt(33)
	v_mul_f32_e32 v14, 0x43800000, v62
	s_waitcnt vmcnt(32)
	v_mul_f32_e32 v4, 0x43800000, v54
	v_med3_f32 v6, v14, s0, v1
	v_med3_f32 v4, v4, s0, v1
	v_cvt_pk_fp8_f32 v135, v6, v4 op_sel:[0,0,1]
	s_waitcnt vmcnt(31)
	v_mul_f32_e32 v4, 0x43800000, v74
	s_waitcnt vmcnt(30)
	v_mul_f32_e32 v6, 0x43800000, v78
	v_med3_f32 v4, v4, s0, v1
	v_med3_f32 v6, v6, s0, v1
	v_mov_b32_e32 v136, v5
	v_cvt_pk_fp8_f32 v136, v4, v6
	s_waitcnt vmcnt(29)
	v_mul_f32_e32 v14, 0x43800000, v102
	s_waitcnt vmcnt(28)
	v_mul_f32_e32 v4, 0x43800000, v86
	v_med3_f32 v6, v14, s0, v1
	v_med3_f32 v4, v4, s0, v1
	v_cvt_pk_fp8_f32 v136, v6, v4 op_sel:[0,0,1]
	s_waitcnt vmcnt(27)
	v_mul_f32_e32 v4, 0x43800000, v106
	s_waitcnt vmcnt(26)
	v_mul_f32_e32 v6, 0x43800000, v114
	v_med3_f32 v4, v4, s0, v1
	v_med3_f32 v6, v6, s0, v1
	v_mov_b32_e32 v137, v5
	v_cvt_pk_fp8_f32 v137, v4, v6
	s_waitcnt vmcnt(25)
	v_mul_f32_e32 v14, 0x43800000, v130
	s_waitcnt vmcnt(24)
	v_mul_f32_e32 v4, 0x43800000, v122
	v_med3_f32 v6, v14, s0, v1
	v_med3_f32 v4, v4, s0, v1
	v_cvt_pk_fp8_f32 v137, v6, v4 op_sel:[0,0,1]
	v_mul_f32_e32 v4, 0x43800000, v7
	v_mul_f32_e32 v6, 0x43800000, v15
	v_med3_f32 v4, v4, s0, v1
	v_med3_f32 v6, v6, s0, v1
	v_mov_b32_e32 v138, v5
	v_cvt_pk_fp8_f32 v138, v4, v6
	v_mul_f32_e32 v7, 0x43800000, v31
	v_mul_f32_e32 v4, 0x43800000, v23
	v_med3_f32 v6, v7, s0, v1
	v_med3_f32 v4, v4, s0, v1
	v_cvt_pk_fp8_f32 v138, v6, v4 op_sel:[0,0,1]
	v_mul_f32_e32 v4, 0x43800000, v43
	v_mul_f32_e32 v6, 0x43800000, v47
	v_med3_f32 v4, v4, s0, v1
	v_med3_f32 v6, v6, s0, v1
	v_mov_b32_e32 v139, v5
	v_cvt_pk_fp8_f32 v139, v4, v6
	v_mul_f32_e32 v7, 0x43800000, v63
	v_mul_f32_e32 v4, 0x43800000, v55
	v_med3_f32 v6, v7, s0, v1
	v_med3_f32 v4, v4, s0, v1
	v_cvt_pk_fp8_f32 v139, v6, v4 op_sel:[0,0,1]
	v_mul_f32_e32 v4, 0x43800000, v75
	v_mul_f32_e32 v6, 0x43800000, v79
	v_med3_f32 v4, v4, s0, v1
	v_med3_f32 v6, v6, s0, v1
	v_mov_b32_e32 v140, v5
	v_cvt_pk_fp8_f32 v140, v4, v6
	v_mul_f32_e32 v7, 0x43800000, v103
	v_mul_f32_e32 v4, 0x43800000, v87
	v_med3_f32 v6, v7, s0, v1
	v_med3_f32 v4, v4, s0, v1
	v_cvt_pk_fp8_f32 v140, v6, v4 op_sel:[0,0,1]
	v_mul_f32_e32 v4, 0x43800000, v107
	v_mul_f32_e32 v6, 0x43800000, v115
	v_med3_f32 v4, v4, s0, v1
	v_med3_f32 v6, v6, s0, v1
	v_mov_b32_e32 v141, v5
	v_cvt_pk_fp8_f32 v141, v4, v6
	v_mul_f32_e32 v7, 0x43800000, v131
	v_mul_f32_e32 v4, 0x43800000, v123
	v_med3_f32 v6, v7, s0, v1
	v_med3_f32 v4, v4, s0, v1
	v_cvt_pk_fp8_f32 v141, v6, v4 op_sel:[0,0,1]
	v_mul_f32_e32 v4, 0x43800000, v8
	v_mul_f32_e32 v6, 0x43800000, v16
	v_med3_f32 v4, v4, s0, v1
	v_med3_f32 v6, v6, s0, v1
	v_mov_b32_e32 v142, v5
	v_cvt_pk_fp8_f32 v142, v4, v6
	v_mul_f32_e32 v7, 0x43800000, v32
	v_mul_f32_e32 v4, 0x43800000, v24
	v_med3_f32 v6, v7, s0, v1
	v_med3_f32 v4, v4, s0, v1
	v_cvt_pk_fp8_f32 v142, v6, v4 op_sel:[0,0,1]
	v_mul_f32_e32 v4, 0x43800000, v44
	v_mul_f32_e32 v6, 0x43800000, v48
	v_med3_f32 v4, v4, s0, v1
	v_med3_f32 v6, v6, s0, v1
	v_mov_b32_e32 v143, v5
	v_cvt_pk_fp8_f32 v143, v4, v6
	v_mul_f32_e32 v7, 0x43800000, v64
	v_mul_f32_e32 v4, 0x43800000, v56
	v_med3_f32 v6, v7, s0, v1
	v_med3_f32 v4, v4, s0, v1
	v_cvt_pk_fp8_f32 v143, v6, v4 op_sel:[0,0,1]
	v_mul_f32_e32 v4, 0x43800000, v76
	v_mul_f32_e32 v6, 0x43800000, v80
	v_med3_f32 v4, v4, s0, v1
	v_med3_f32 v6, v6, s0, v1
	v_mov_b32_e32 v144, v5
	v_cvt_pk_fp8_f32 v144, v4, v6
	v_mul_f32_e32 v7, 0x43800000, v104
	v_mul_f32_e32 v4, 0x43800000, v88
	v_med3_f32 v6, v7, s0, v1
	v_med3_f32 v4, v4, s0, v1
	v_cvt_pk_fp8_f32 v144, v6, v4 op_sel:[0,0,1]
	v_mul_f32_e32 v4, 0x43800000, v108
	v_mul_f32_e32 v6, 0x43800000, v116
	v_med3_f32 v4, v4, s0, v1
	v_med3_f32 v6, v6, s0, v1
	v_mov_b32_e32 v145, v5
	v_cvt_pk_fp8_f32 v145, v4, v6
	v_mul_f32_e32 v7, 0x43800000, v132
	v_mul_f32_e32 v4, 0x43800000, v124
	v_med3_f32 v6, v7, s0, v1
	v_med3_f32 v4, v4, s0, v1
	v_cvt_pk_fp8_f32 v145, v6, v4 op_sel:[0,0,1]
	v_mul_f32_e32 v4, 0x43800000, v9
	v_mul_f32_e32 v6, 0x43800000, v17
	v_med3_f32 v4, v4, s0, v1
	v_med3_f32 v8, v6, s0, v1
	v_mov_b32_e32 v6, v5
	v_cvt_pk_fp8_f32 v6, v4, v8
	v_mul_f32_e32 v7, 0x43800000, v33
	v_mul_f32_e32 v4, 0x43800000, v25
	v_med3_f32 v7, v7, s0, v1
	v_med3_f32 v4, v4, s0, v1
	v_cvt_pk_fp8_f32 v6, v7, v4 op_sel:[0,0,1]
	v_mul_f32_e32 v4, 0x43800000, v45
	v_mul_f32_e32 v7, 0x43800000, v49
	v_med3_f32 v4, v4, s0, v1
	v_med3_f32 v9, v7, s0, v1
	v_mov_b32_e32 v7, v5
	v_cvt_pk_fp8_f32 v7, v4, v9
	v_mul_f32_e32 v8, 0x43800000, v65
	v_mul_f32_e32 v4, 0x43800000, v57
	v_med3_f32 v8, v8, s0, v1
	v_med3_f32 v4, v4, s0, v1
	v_cvt_pk_fp8_f32 v7, v8, v4 op_sel:[0,0,1]
	v_mul_f32_e32 v4, 0x43800000, v77
	v_mul_f32_e32 v8, 0x43800000, v81
	v_med3_f32 v4, v4, s0, v1
	v_med3_f32 v14, v8, s0, v1
	v_mov_b32_e32 v8, v5
	v_cvt_pk_fp8_f32 v8, v4, v14
	v_mul_f32_e32 v9, 0x43800000, v105
	v_mul_f32_e32 v4, 0x43800000, v89
	v_med3_f32 v9, v9, s0, v1
	v_med3_f32 v4, v4, s0, v1
	v_cvt_pk_fp8_f32 v8, v9, v4 op_sel:[0,0,1]
	v_mul_f32_e32 v4, 0x43800000, v109
	v_mul_f32_e32 v9, 0x43800000, v117
	v_med3_f32 v4, v4, s0, v1
	v_med3_f32 v15, v9, s0, v1
	v_mov_b32_e32 v9, v5
	v_cvt_pk_fp8_f32 v9, v4, v15
	v_mul_f32_e32 v14, 0x43800000, v133
	v_mul_f32_e32 v4, 0x43800000, v125
	v_med3_f32 v14, v14, s0, v1
	v_med3_f32 v4, v4, s0, v1
	v_cvt_pk_fp8_f32 v9, v14, v4 op_sel:[0,0,1]
	ds_write_b128 v166, v[134:137] offset:34816
	ds_write_b128 v166, v[138:141] offset:35088
	ds_write_b128 v166, v[142:145] offset:35360
	ds_write_b128 v166, v[6:9] offset:35632
	s_waitcnt lgkmcnt(0)
	s_barrier
	s_mov_b32 s1, 0xe00000
	v_add_co_u32_e32 v6, vcc, s1, v2
	s_mov_b32 s1, 0xe02000
	s_nop 0
	v_addc_co_u32_e32 v7, vcc, 0, v3, vcc
	v_add_co_u32_e32 v14, vcc, s1, v2
	s_mov_b32 s1, 0xe04000
	s_nop 0
	v_addc_co_u32_e32 v15, vcc, 0, v3, vcc
	v_add_co_u32_e32 v42, vcc, s1, v2
	s_mov_b32 s1, 0xe06000
	s_nop 0
	v_addc_co_u32_e32 v43, vcc, 0, v3, vcc
	v_add_co_u32_e32 v44, vcc, s1, v2
	s_mov_b32 s1, 0xe08000
	s_nop 0
	v_addc_co_u32_e32 v45, vcc, 0, v3, vcc
	v_add_co_u32_e32 v54, vcc, s1, v2
	s_mov_b32 s1, 0xe0a000
	s_nop 0
	v_addc_co_u32_e32 v55, vcc, 0, v3, vcc
	v_add_co_u32_e32 v56, vcc, s1, v2
	s_mov_b32 s1, 0xe0c000
	s_nop 0
	v_addc_co_u32_e32 v57, vcc, 0, v3, vcc
	v_add_co_u32_e32 v74, vcc, s1, v2
	s_mov_b32 s1, 0xe0e000
	s_nop 0
	v_addc_co_u32_e32 v75, vcc, 0, v3, vcc
	v_add_co_u32_e32 v76, vcc, s1, v2
	s_mov_b32 s1, 0xe10000
	s_nop 0
	v_addc_co_u32_e32 v77, vcc, 0, v3, vcc
	v_add_co_u32_e32 v86, vcc, s1, v2
	s_mov_b32 s1, 0xe12000
	s_nop 0
	v_addc_co_u32_e32 v87, vcc, 0, v3, vcc
	v_add_co_u32_e32 v88, vcc, s1, v2
	s_mov_b32 s1, 0xe14000
	s_nop 0
	v_addc_co_u32_e32 v89, vcc, 0, v3, vcc
	global_load_dwordx4 v[6:9], v[6:7], off sc0 nt
	s_nop 0
	global_load_dwordx4 v[14:17], v[14:15], off sc0 nt
	s_nop 0
	global_load_dwordx4 v[30:33], v[42:43], off sc0 nt
	global_load_dwordx4 v[22:25], v[44:45], off sc0 nt
	s_nop 0
	global_load_dwordx4 v[42:45], v[54:55], off sc0 nt
	global_load_dwordx4 v[46:49], v[56:57], off sc0 nt
	global_load_dwordx4 v[62:65], v[74:75], off sc0 nt
	s_nop 0
	global_load_dwordx4 v[54:57], v[76:77], off sc0 nt
	s_nop 0
	global_load_dwordx4 v[74:77], v[86:87], off sc0 nt
	global_load_dwordx4 v[78:81], v[88:89], off sc0 nt
	v_add_co_u32_e32 v86, vcc, s1, v2
	s_mov_b32 s1, 0xe16000
	s_nop 0
	v_addc_co_u32_e32 v87, vcc, 0, v3, vcc
	v_add_co_u32_e32 v88, vcc, s1, v2
	s_mov_b32 s1, 0xe18000
	s_nop 0
	v_addc_co_u32_e32 v89, vcc, 0, v3, vcc
	v_add_co_u32_e32 v106, vcc, s1, v2
	s_mov_b32 s1, 0xe1a000
	s_nop 0
	v_addc_co_u32_e32 v107, vcc, 0, v3, vcc
	v_add_co_u32_e32 v114, vcc, s1, v2
	s_mov_b32 s1, 0xe1c000
	s_nop 0
	v_addc_co_u32_e32 v115, vcc, 0, v3, vcc
	v_add_co_u32_e32 v122, vcc, s1, v2
	s_mov_b32 s1, 0xe1e000
	s_nop 0
	v_addc_co_u32_e32 v123, vcc, 0, v3, vcc
	v_add_co_u32_e32 v2, vcc, s1, v2
	global_load_dwordx4 v[102:105], v[86:87], off sc0 nt
	s_nop 0
	global_load_dwordx4 v[86:89], v[88:89], off sc0 nt
	s_nop 0
	global_load_dwordx4 v[106:109], v[106:107], off sc0 nt
	s_nop 0
	global_load_dwordx4 v[114:117], v[114:115], off sc0 nt
	v_addc_co_u32_e32 v3, vcc, 0, v3, vcc
	global_load_dwordx4 v[130:133], v[122:123], off sc0 nt
	s_nop 0
	global_load_dwordx4 v[122:125], v[2:3], off sc0 nt
	ds_read_b128 v[134:137], v154 offset:34816
	ds_read_b128 v[138:141], v156 offset:34816
	ds_read_b128 v[142:145], v158 offset:34816
	ds_read_b128 v[146:149], v162 offset:34816
	s_waitcnt lgkmcnt(3)
	global_store_dwordx4 v[150:151], v[134:137], off offset:1280 nt
	s_waitcnt lgkmcnt(2)
	global_store_dwordx4 v[152:153], v[138:141], off offset:1280 nt
	s_waitcnt lgkmcnt(1)
	global_store_dwordx4 v[160:161], v[142:145], off offset:1280 nt
	s_waitcnt lgkmcnt(0)
	global_store_dwordx4 v[164:165], v[146:149], off offset:1280 nt
	s_waitcnt vmcnt(39)
	v_mul_f32_e32 v2, 0x43800000, v10
	s_waitcnt vmcnt(38)
	v_mul_f32_e32 v3, 0x43800000, v18
	v_med3_f32 v2, v2, s0, v1
	v_med3_f32 v3, v3, s0, v1
	v_mov_b32_e32 v134, v5
	v_cvt_pk_fp8_f32 v134, v2, v3
	s_waitcnt vmcnt(37)
	v_mul_f32_e32 v4, 0x43800000, v34
	s_waitcnt vmcnt(36)
	v_mul_f32_e32 v2, 0x43800000, v26
	v_med3_f32 v3, v4, s0, v1
	v_med3_f32 v2, v2, s0, v1
	v_cvt_pk_fp8_f32 v134, v3, v2 op_sel:[0,0,1]
	s_waitcnt vmcnt(35)
	v_mul_f32_e32 v2, 0x43800000, v38
	s_waitcnt vmcnt(34)
	v_mul_f32_e32 v3, 0x43800000, v50
	v_med3_f32 v2, v2, s0, v1
	v_med3_f32 v3, v3, s0, v1
	v_mov_b32_e32 v135, v5
	v_cvt_pk_fp8_f32 v135, v2, v3
	s_waitcnt vmcnt(33)
	v_mul_f32_e32 v4, 0x43800000, v66
	s_waitcnt vmcnt(32)
	v_mul_f32_e32 v2, 0x43800000, v58
	v_med3_f32 v3, v4, s0, v1
	v_med3_f32 v2, v2, s0, v1
	v_cvt_pk_fp8_f32 v135, v3, v2 op_sel:[0,0,1]
	s_waitcnt vmcnt(31)
	v_mul_f32_e32 v2, 0x43800000, v70
	s_waitcnt vmcnt(30)
	v_mul_f32_e32 v3, 0x43800000, v82
	v_med3_f32 v2, v2, s0, v1
	v_med3_f32 v3, v3, s0, v1
	v_mov_b32_e32 v136, v5
	v_cvt_pk_fp8_f32 v136, v2, v3
	s_waitcnt vmcnt(29)
	v_mul_f32_e32 v4, 0x43800000, v94
	s_waitcnt vmcnt(28)
	v_mul_f32_e32 v2, 0x43800000, v90
	v_med3_f32 v3, v4, s0, v1
	v_med3_f32 v2, v2, s0, v1
	v_cvt_pk_fp8_f32 v136, v3, v2 op_sel:[0,0,1]
	s_waitcnt vmcnt(27)
	v_mul_f32_e32 v2, 0x43800000, v98
	s_waitcnt vmcnt(26)
	v_mul_f32_e32 v3, 0x43800000, v110
	v_med3_f32 v2, v2, s0, v1
	v_med3_f32 v3, v3, s0, v1
	v_mov_b32_e32 v137, v5
	v_cvt_pk_fp8_f32 v137, v2, v3
	s_waitcnt vmcnt(25)
	v_mul_f32_e32 v4, 0x43800000, v126
	s_waitcnt vmcnt(24)
	v_mul_f32_e32 v2, 0x43800000, v118
	v_med3_f32 v3, v4, s0, v1
	v_med3_f32 v2, v2, s0, v1
	v_cvt_pk_fp8_f32 v137, v3, v2 op_sel:[0,0,1]
	v_mul_f32_e32 v2, 0x43800000, v11
	v_mul_f32_e32 v3, 0x43800000, v19
	v_med3_f32 v2, v2, s0, v1
	v_med3_f32 v3, v3, s0, v1
	v_mov_b32_e32 v138, v5
	v_cvt_pk_fp8_f32 v138, v2, v3
	v_mul_f32_e32 v4, 0x43800000, v35
	v_mul_f32_e32 v2, 0x43800000, v27
	v_med3_f32 v3, v4, s0, v1
	v_med3_f32 v2, v2, s0, v1
	v_cvt_pk_fp8_f32 v138, v3, v2 op_sel:[0,0,1]
	v_mul_f32_e32 v2, 0x43800000, v39
	v_mul_f32_e32 v3, 0x43800000, v51
	v_med3_f32 v2, v2, s0, v1
	v_med3_f32 v3, v3, s0, v1
	v_mov_b32_e32 v139, v5
	v_cvt_pk_fp8_f32 v139, v2, v3
	v_mul_f32_e32 v4, 0x43800000, v67
	v_mul_f32_e32 v2, 0x43800000, v59
	v_med3_f32 v3, v4, s0, v1
	v_med3_f32 v2, v2, s0, v1
	v_cvt_pk_fp8_f32 v139, v3, v2 op_sel:[0,0,1]
	v_mul_f32_e32 v2, 0x43800000, v71
	v_mul_f32_e32 v3, 0x43800000, v83
	v_med3_f32 v2, v2, s0, v1
	v_med3_f32 v3, v3, s0, v1
	v_mov_b32_e32 v140, v5
	v_cvt_pk_fp8_f32 v140, v2, v3
	v_mul_f32_e32 v4, 0x43800000, v95
	v_mul_f32_e32 v2, 0x43800000, v91
	v_med3_f32 v3, v4, s0, v1
	v_med3_f32 v2, v2, s0, v1
	v_cvt_pk_fp8_f32 v140, v3, v2 op_sel:[0,0,1]
	v_mul_f32_e32 v2, 0x43800000, v99
	v_mul_f32_e32 v3, 0x43800000, v111
	v_med3_f32 v2, v2, s0, v1
	v_med3_f32 v3, v3, s0, v1
	v_mov_b32_e32 v141, v5
	v_cvt_pk_fp8_f32 v141, v2, v3
	v_mul_f32_e32 v4, 0x43800000, v127
	v_mul_f32_e32 v2, 0x43800000, v119
	v_med3_f32 v3, v4, s0, v1
	v_med3_f32 v2, v2, s0, v1
	v_cvt_pk_fp8_f32 v141, v3, v2 op_sel:[0,0,1]
	v_mul_f32_e32 v2, 0x43800000, v12
	v_mul_f32_e32 v3, 0x43800000, v20
	v_med3_f32 v2, v2, s0, v1
	v_med3_f32 v3, v3, s0, v1
	v_mov_b32_e32 v142, v5
	v_cvt_pk_fp8_f32 v142, v2, v3
	v_mul_f32_e32 v4, 0x43800000, v36
	v_mul_f32_e32 v2, 0x43800000, v28
	v_med3_f32 v3, v4, s0, v1
	v_med3_f32 v2, v2, s0, v1
	v_cvt_pk_fp8_f32 v142, v3, v2 op_sel:[0,0,1]
	v_mul_f32_e32 v2, 0x43800000, v40
	v_mul_f32_e32 v3, 0x43800000, v52
	v_med3_f32 v2, v2, s0, v1
	v_med3_f32 v3, v3, s0, v1
	v_mov_b32_e32 v143, v5
	v_cvt_pk_fp8_f32 v143, v2, v3
	v_mul_f32_e32 v4, 0x43800000, v68
	v_mul_f32_e32 v2, 0x43800000, v60
	v_med3_f32 v3, v4, s0, v1
	v_med3_f32 v2, v2, s0, v1
	v_cvt_pk_fp8_f32 v143, v3, v2 op_sel:[0,0,1]
	v_mul_f32_e32 v2, 0x43800000, v72
	v_mul_f32_e32 v3, 0x43800000, v84
	v_med3_f32 v2, v2, s0, v1
	v_med3_f32 v3, v3, s0, v1
	v_mov_b32_e32 v144, v5
	v_cvt_pk_fp8_f32 v144, v2, v3
	v_mul_f32_e32 v4, 0x43800000, v96
	v_mul_f32_e32 v2, 0x43800000, v92
	v_med3_f32 v3, v4, s0, v1
	v_med3_f32 v2, v2, s0, v1
	v_cvt_pk_fp8_f32 v144, v3, v2 op_sel:[0,0,1]
	v_mul_f32_e32 v2, 0x43800000, v100
	v_mul_f32_e32 v3, 0x43800000, v112
	v_med3_f32 v2, v2, s0, v1
	v_med3_f32 v3, v3, s0, v1
	v_mov_b32_e32 v145, v5
	v_cvt_pk_fp8_f32 v145, v2, v3
	v_mul_f32_e32 v4, 0x43800000, v128
	v_mul_f32_e32 v2, 0x43800000, v120
	v_med3_f32 v3, v4, s0, v1
	v_med3_f32 v2, v2, s0, v1
	v_cvt_pk_fp8_f32 v145, v3, v2 op_sel:[0,0,1]
	v_mul_f32_e32 v2, 0x43800000, v13
	v_mul_f32_e32 v3, 0x43800000, v21
	v_med3_f32 v2, v2, s0, v1
	v_med3_f32 v3, v3, s0, v1
	v_mov_b32_e32 v10, v5
	v_cvt_pk_fp8_f32 v10, v2, v3
	v_mul_f32_e32 v4, 0x43800000, v37
	v_mul_f32_e32 v2, 0x43800000, v29
	v_med3_f32 v3, v4, s0, v1
	v_med3_f32 v2, v2, s0, v1
	v_cvt_pk_fp8_f32 v10, v3, v2 op_sel:[0,0,1]
	v_mul_f32_e32 v2, 0x43800000, v41
	v_mul_f32_e32 v3, 0x43800000, v53
	v_med3_f32 v2, v2, s0, v1
	v_med3_f32 v3, v3, s0, v1
	v_mov_b32_e32 v11, v5
	v_cvt_pk_fp8_f32 v11, v2, v3
	v_mul_f32_e32 v4, 0x43800000, v69
	v_mul_f32_e32 v2, 0x43800000, v61
	v_med3_f32 v3, v4, s0, v1
	v_med3_f32 v2, v2, s0, v1
	v_cvt_pk_fp8_f32 v11, v3, v2 op_sel:[0,0,1]
	v_mul_f32_e32 v2, 0x43800000, v73
	v_mul_f32_e32 v3, 0x43800000, v85
	v_med3_f32 v2, v2, s0, v1
	v_med3_f32 v3, v3, s0, v1
	v_mov_b32_e32 v12, v5
	v_cvt_pk_fp8_f32 v12, v2, v3
	v_mul_f32_e32 v4, 0x43800000, v97
	v_mul_f32_e32 v2, 0x43800000, v93
	v_med3_f32 v3, v4, s0, v1
	v_med3_f32 v2, v2, s0, v1
	v_cvt_pk_fp8_f32 v12, v3, v2 op_sel:[0,0,1]
	v_mul_f32_e32 v2, 0x43800000, v101
	v_mul_f32_e32 v3, 0x43800000, v113
	v_med3_f32 v2, v2, s0, v1
	v_med3_f32 v3, v3, s0, v1
	v_mov_b32_e32 v13, v5
	v_cvt_pk_fp8_f32 v13, v2, v3
	v_mul_f32_e32 v4, 0x43800000, v129
	v_mul_f32_e32 v2, 0x43800000, v121
	v_med3_f32 v3, v4, s0, v1
	v_med3_f32 v2, v2, s0, v1
	v_cvt_pk_fp8_f32 v13, v3, v2 op_sel:[0,0,1]
	ds_write_b128 v166, v[134:137]
	ds_write_b128 v166, v[138:141] offset:272
	ds_write_b128 v166, v[142:145] offset:544
	ds_write_b128 v166, v[10:13] offset:816
	s_waitcnt lgkmcnt(0)
	s_barrier
	ds_read_b128 v[10:13], v154
	ds_read_b128 v[18:21], v156
	ds_read_b128 v[26:29], v158
	ds_read_b128 v[34:37], v162
	s_waitcnt lgkmcnt(3)
	global_store_dwordx4 v[150:151], v[10:13], off offset:1536 nt
	s_waitcnt lgkmcnt(2)
	global_store_dwordx4 v[152:153], v[18:21], off offset:1536 nt
	s_waitcnt lgkmcnt(1)
	global_store_dwordx4 v[160:161], v[26:29], off offset:1536 nt
	s_waitcnt lgkmcnt(0)
	global_store_dwordx4 v[164:165], v[34:37], off offset:1536 nt
	s_waitcnt vmcnt(23)
	v_mul_f32_e32 v2, 0x43800000, v6
	s_waitcnt vmcnt(22)
	v_mul_f32_e32 v3, 0x43800000, v14
	v_med3_f32 v2, v2, s0, v1
	v_med3_f32 v3, v3, s0, v1
	v_mov_b32_e32 v10, v5
	v_cvt_pk_fp8_f32 v10, v2, v3
	s_waitcnt vmcnt(21)
	v_mul_f32_e32 v4, 0x43800000, v30
	s_waitcnt vmcnt(20)
	v_mul_f32_e32 v2, 0x43800000, v22
	v_med3_f32 v3, v4, s0, v1
	v_med3_f32 v2, v2, s0, v1
	v_cvt_pk_fp8_f32 v10, v3, v2 op_sel:[0,0,1]
	s_waitcnt vmcnt(19)
	v_mul_f32_e32 v2, 0x43800000, v42
	s_waitcnt vmcnt(18)
	v_mul_f32_e32 v3, 0x43800000, v46
	v_med3_f32 v2, v2, s0, v1
	v_med3_f32 v3, v3, s0, v1
	v_mov_b32_e32 v11, v5
	v_cvt_pk_fp8_f32 v11, v2, v3
	s_waitcnt vmcnt(17)
	v_mul_f32_e32 v4, 0x43800000, v62
	s_waitcnt vmcnt(16)
	v_mul_f32_e32 v2, 0x43800000, v54
	v_med3_f32 v3, v4, s0, v1
	v_med3_f32 v2, v2, s0, v1
	v_cvt_pk_fp8_f32 v11, v3, v2 op_sel:[0,0,1]
	s_waitcnt vmcnt(15)
	v_mul_f32_e32 v2, 0x43800000, v74
	s_waitcnt vmcnt(14)
	v_mul_f32_e32 v3, 0x43800000, v78
	v_med3_f32 v2, v2, s0, v1
	v_med3_f32 v3, v3, s0, v1
	v_mov_b32_e32 v12, v5
	v_cvt_pk_fp8_f32 v12, v2, v3
	s_waitcnt vmcnt(13)
	v_mul_f32_e32 v4, 0x43800000, v102
	s_waitcnt vmcnt(12)
	v_mul_f32_e32 v2, 0x43800000, v86
	v_med3_f32 v3, v4, s0, v1
	v_med3_f32 v2, v2, s0, v1
	v_cvt_pk_fp8_f32 v12, v3, v2 op_sel:[0,0,1]
	s_waitcnt vmcnt(11)
	v_mul_f32_e32 v2, 0x43800000, v106
	s_waitcnt vmcnt(10)
	v_mul_f32_e32 v3, 0x43800000, v114
	v_med3_f32 v2, v2, s0, v1
	v_med3_f32 v3, v3, s0, v1
	v_mov_b32_e32 v13, v5
	v_cvt_pk_fp8_f32 v13, v2, v3
	s_waitcnt vmcnt(9)
	v_mul_f32_e32 v4, 0x43800000, v130
	s_waitcnt vmcnt(8)
	v_mul_f32_e32 v2, 0x43800000, v122
	v_med3_f32 v3, v4, s0, v1
	v_med3_f32 v2, v2, s0, v1
	v_cvt_pk_fp8_f32 v13, v3, v2 op_sel:[0,0,1]
	v_mul_f32_e32 v2, 0x43800000, v7
	v_mul_f32_e32 v3, 0x43800000, v15
	v_med3_f32 v2, v2, s0, v1
	v_med3_f32 v3, v3, s0, v1
	v_mov_b32_e32 v18, v5
	v_cvt_pk_fp8_f32 v18, v2, v3
	v_mul_f32_e32 v4, 0x43800000, v31
	v_mul_f32_e32 v2, 0x43800000, v23
	v_med3_f32 v3, v4, s0, v1
	v_med3_f32 v2, v2, s0, v1
	v_cvt_pk_fp8_f32 v18, v3, v2 op_sel:[0,0,1]
	v_mul_f32_e32 v2, 0x43800000, v43
	v_mul_f32_e32 v3, 0x43800000, v47
	v_med3_f32 v2, v2, s0, v1
	v_med3_f32 v3, v3, s0, v1
	v_mov_b32_e32 v19, v5
	v_cvt_pk_fp8_f32 v19, v2, v3
	v_mul_f32_e32 v4, 0x43800000, v63
	v_mul_f32_e32 v2, 0x43800000, v55
	v_med3_f32 v3, v4, s0, v1
	v_med3_f32 v2, v2, s0, v1
	v_cvt_pk_fp8_f32 v19, v3, v2 op_sel:[0,0,1]
	v_mul_f32_e32 v2, 0x43800000, v75
	v_mul_f32_e32 v3, 0x43800000, v79
	v_med3_f32 v2, v2, s0, v1
	v_med3_f32 v3, v3, s0, v1
	v_mov_b32_e32 v20, v5
	v_cvt_pk_fp8_f32 v20, v2, v3
	v_mul_f32_e32 v4, 0x43800000, v103
	v_mul_f32_e32 v2, 0x43800000, v87
	v_med3_f32 v3, v4, s0, v1
	v_med3_f32 v2, v2, s0, v1
	v_cvt_pk_fp8_f32 v20, v3, v2 op_sel:[0,0,1]
	v_mul_f32_e32 v2, 0x43800000, v107
	v_mul_f32_e32 v3, 0x43800000, v115
	v_med3_f32 v2, v2, s0, v1
	v_med3_f32 v3, v3, s0, v1
	v_mov_b32_e32 v21, v5
	v_cvt_pk_fp8_f32 v21, v2, v3
	v_mul_f32_e32 v4, 0x43800000, v131
	v_mul_f32_e32 v2, 0x43800000, v123
	v_med3_f32 v3, v4, s0, v1
	v_med3_f32 v2, v2, s0, v1
	v_cvt_pk_fp8_f32 v21, v3, v2 op_sel:[0,0,1]
	v_mul_f32_e32 v2, 0x43800000, v8
	v_mul_f32_e32 v3, 0x43800000, v16
	v_med3_f32 v2, v2, s0, v1
	v_med3_f32 v3, v3, s0, v1
	v_mov_b32_e32 v26, v5
	v_cvt_pk_fp8_f32 v26, v2, v3
	v_mul_f32_e32 v4, 0x43800000, v32
	v_mul_f32_e32 v2, 0x43800000, v24
	v_med3_f32 v3, v4, s0, v1
	v_med3_f32 v2, v2, s0, v1
	v_cvt_pk_fp8_f32 v26, v3, v2 op_sel:[0,0,1]
	v_mul_f32_e32 v2, 0x43800000, v44
	v_mul_f32_e32 v3, 0x43800000, v48
	v_med3_f32 v2, v2, s0, v1
	v_med3_f32 v3, v3, s0, v1
	v_mov_b32_e32 v27, v5
	v_cvt_pk_fp8_f32 v27, v2, v3
	v_mul_f32_e32 v4, 0x43800000, v64
	v_mul_f32_e32 v2, 0x43800000, v56
	v_med3_f32 v3, v4, s0, v1
	v_med3_f32 v2, v2, s0, v1
	v_cvt_pk_fp8_f32 v27, v3, v2 op_sel:[0,0,1]
	v_mul_f32_e32 v2, 0x43800000, v76
	v_mul_f32_e32 v3, 0x43800000, v80
	v_med3_f32 v2, v2, s0, v1
	v_med3_f32 v3, v3, s0, v1
	v_mov_b32_e32 v28, v5
	v_cvt_pk_fp8_f32 v28, v2, v3
	v_mul_f32_e32 v4, 0x43800000, v104
	v_mul_f32_e32 v2, 0x43800000, v88
	v_med3_f32 v3, v4, s0, v1
	v_med3_f32 v2, v2, s0, v1
	v_cvt_pk_fp8_f32 v28, v3, v2 op_sel:[0,0,1]
	v_mul_f32_e32 v2, 0x43800000, v108
	v_mul_f32_e32 v3, 0x43800000, v116
	v_med3_f32 v2, v2, s0, v1
	v_med3_f32 v3, v3, s0, v1
	v_mov_b32_e32 v29, v5
	v_cvt_pk_fp8_f32 v29, v2, v3
	v_mul_f32_e32 v4, 0x43800000, v132
	v_mul_f32_e32 v2, 0x43800000, v124
	v_med3_f32 v3, v4, s0, v1
	v_med3_f32 v2, v2, s0, v1
	v_cvt_pk_fp8_f32 v29, v3, v2 op_sel:[0,0,1]
	v_mul_f32_e32 v2, 0x43800000, v9
	v_mul_f32_e32 v3, 0x43800000, v17
	v_med3_f32 v6, v2, s0, v1
	v_med3_f32 v3, v3, s0, v1
	v_mov_b32_e32 v2, v5
	v_cvt_pk_fp8_f32 v2, v6, v3
	v_mul_f32_e32 v4, 0x43800000, v33
	v_mul_f32_e32 v3, 0x43800000, v25
	v_med3_f32 v4, v4, s0, v1
	v_med3_f32 v3, v3, s0, v1
	v_cvt_pk_fp8_f32 v2, v4, v3 op_sel:[0,0,1]
	v_mul_f32_e32 v3, 0x43800000, v45
	v_mul_f32_e32 v4, 0x43800000, v49
	v_med3_f32 v7, v3, s0, v1
	v_med3_f32 v4, v4, s0, v1
	v_mov_b32_e32 v3, v5
	v_cvt_pk_fp8_f32 v3, v7, v4
	v_mul_f32_e32 v6, 0x43800000, v65
	v_mul_f32_e32 v4, 0x43800000, v57
	v_med3_f32 v6, v6, s0, v1
	v_med3_f32 v4, v4, s0, v1
	v_cvt_pk_fp8_f32 v3, v6, v4 op_sel:[0,0,1]
	v_mul_f32_e32 v4, 0x43800000, v77
	v_mul_f32_e32 v6, 0x43800000, v81
	v_med3_f32 v8, v4, s0, v1
	v_med3_f32 v6, v6, s0, v1
	v_mov_b32_e32 v4, v5
	v_cvt_pk_fp8_f32 v4, v8, v6
	v_mul_f32_e32 v7, 0x43800000, v105
	v_mul_f32_e32 v6, 0x43800000, v89
	v_med3_f32 v7, v7, s0, v1
	v_med3_f32 v6, v6, s0, v1
	v_cvt_pk_fp8_f32 v4, v7, v6 op_sel:[0,0,1]
	v_mul_f32_e32 v6, 0x43800000, v109
	v_mul_f32_e32 v7, 0x43800000, v117
	v_med3_f32 v6, v6, s0, v1
	v_med3_f32 v7, v7, s0, v1
	v_cvt_pk_fp8_f32 v5, v6, v7
	v_mul_f32_e32 v8, 0x43800000, v133
	v_mul_f32_e32 v6, 0x43800000, v125
	v_med3_f32 v7, v8, s0, v1
	v_med3_f32 v1, v6, s0, v1
	v_cvt_pk_fp8_f32 v5, v7, v1 op_sel:[0,0,1]
	ds_write_b128 v166, v[10:13] offset:34816
	ds_write_b128 v166, v[18:21] offset:35088
	ds_write_b128 v166, v[26:29] offset:35360
	ds_write_b128 v166, v[2:5] offset:35632
	s_waitcnt lgkmcnt(0)
	s_barrier
	ds_read_b128 v[2:5], v154 offset:34816
	ds_read_b128 v[6:9], v156 offset:34816
	ds_read_b128 v[10:13], v158 offset:34816
	ds_read_b128 v[14:17], v162 offset:34816
	s_waitcnt lgkmcnt(3)
	global_store_dwordx4 v[150:151], v[2:5], off offset:1792 nt
	s_waitcnt lgkmcnt(2)
	global_store_dwordx4 v[152:153], v[6:9], off offset:1792 nt
	s_waitcnt lgkmcnt(1)
	global_store_dwordx4 v[160:161], v[10:13], off offset:1792 nt
	s_waitcnt lgkmcnt(0)
	global_store_dwordx4 v[164:165], v[14:17], off offset:1792 nt
	s_barrier
	s_mov_b64 s[6:7], 0
.LBB0_1084:
	s_andn2_b64 vcc, exec, s[6:7]
	s_cbranch_vccnz .LBB0_1086
	s_add_i32 s0, s74, 0x400
	s_ashr_i32 s0, s0, 5
	s_ashr_i32 s1, s0, 31
	v_readlane_b32 s12, v254, 4
	s_and_b32 s4, s74, 31
	s_lshl_b64 s[2:3], s[0:1], 25
	v_readlane_b32 s14, v254, 6
	v_readlane_b32 s15, v254, 7
	s_add_u32 s2, s14, s2
	s_addc_u32 s3, s15, s3
	s_lshl_b32 s6, s74, 6
	s_lshl_b32 s7, s74, 11
	s_and_b32 s6, s6, 0x780
	s_and_b32 s7, s7, 0x800
	s_or_b32 s6, s6, s7
	s_lshl_b32 s6, s6, 2
	s_add_u32 s2, s2, s6
	s_addc_u32 s3, s3, 0
	s_lshl_b32 s4, s4, 18
	s_lshl_b64 s[0:1], s[0:1], 23
	s_add_u32 s0, s78, s0
	v_mov_b32_e32 v134, v0
	s_addc_u32 s1, s79, s1
	s_add_u32 s6, s0, s4
	v_readfirstlane_b32 s5, v134
	s_addc_u32 s7, s1, 0
	s_ashr_i32 s0, s5, 1
	v_lshrrev_b32_e32 v1, 1, v134
	s_andn2_b32 s0, s0, 31
	v_and_b32_e32 v135, 16, v1
	v_or_b32_e32 v2, s0, v135
	v_ashrrev_i32_e32 v3, 31, v2
	v_lshlrev_b32_e32 v1, 2, v134
	v_lshlrev_b64 v[2:3], 14, v[2:3]
	v_and_b32_e32 v140, 0x7c, v1
	v_lshl_add_u64 v[2:3], s[2:3], 0, v[2:3]
	v_lshlrev_b32_e32 v4, 2, v140
	v_mov_b32_e32 v5, 0
	v_lshl_add_u64 v[2:3], v[2:3], 0, v[4:5]
	s_movk_i32 s1, 0x4000
	v_add_co_u32_e32 v6, vcc, s1, v2
	s_mov_b32 s1, 0x8000
	s_nop 0
	v_addc_co_u32_e32 v7, vcc, 0, v3, vcc
	global_load_dwordx4 v[34:37], v[2:3], off sc0 nt
	global_load_dwordx4 v[38:41], v[6:7], off sc0 nt
	v_add_co_u32_e32 v6, vcc, s1, v2
	s_mov_b32 s1, 0xc000
	s_nop 0
	v_addc_co_u32_e32 v7, vcc, 0, v3, vcc
	v_add_co_u32_e32 v8, vcc, s1, v2
	s_mov_b32 s1, 0x10000
	s_nop 0
	v_addc_co_u32_e32 v9, vcc, 0, v3, vcc
	global_load_dwordx4 v[58:61], v[6:7], off sc0 nt
	global_load_dwordx4 v[50:53], v[8:9], off sc0 nt
	v_add_co_u32_e32 v6, vcc, s1, v2
	s_mov_b32 s1, 0x14000
	s_nop 0
	v_addc_co_u32_e32 v7, vcc, 0, v3, vcc
	v_add_co_u32_e32 v8, vcc, s1, v2
	s_mov_b32 s1, 0x18000
	s_nop 0
	v_addc_co_u32_e32 v9, vcc, 0, v3, vcc
	global_load_dwordx4 v[66:69], v[6:7], off sc0 nt
	global_load_dwordx4 v[70:73], v[8:9], off sc0 nt
	v_add_co_u32_e32 v6, vcc, s1, v2
	s_mov_b32 s1, 0x1c000
	s_nop 0
	v_addc_co_u32_e32 v7, vcc, 0, v3, vcc
	v_add_co_u32_e32 v8, vcc, s1, v2
	s_mov_b32 s1, 0x20000
	s_nop 0
	v_addc_co_u32_e32 v9, vcc, 0, v3, vcc
	global_load_dwordx4 v[94:97], v[6:7], off sc0 nt
	global_load_dwordx4 v[82:85], v[8:9], off sc0 nt
	v_add_co_u32_e32 v6, vcc, s1, v2
	s_mov_b32 s1, 0x24000
	s_nop 0
	v_addc_co_u32_e32 v7, vcc, 0, v3, vcc
	v_add_co_u32_e32 v8, vcc, s1, v2
	s_mov_b32 s1, 0x28000
	s_nop 0
	v_addc_co_u32_e32 v9, vcc, 0, v3, vcc
	global_load_dwordx4 v[98:101], v[6:7], off sc0 nt
	global_load_dwordx4 v[102:105], v[8:9], off sc0 nt
	v_add_co_u32_e32 v6, vcc, s1, v2
	s_mov_b32 s1, 0x2c000
	s_nop 0
	v_addc_co_u32_e32 v7, vcc, 0, v3, vcc
	v_add_co_u32_e32 v8, vcc, s1, v2
	s_mov_b32 s1, 0x30000
	s_nop 0
	v_addc_co_u32_e32 v9, vcc, 0, v3, vcc
	global_load_dwordx4 v[114:117], v[6:7], off sc0 nt
	global_load_dwordx4 v[110:113], v[8:9], off sc0 nt
	v_add_co_u32_e32 v6, vcc, s1, v2
	s_mov_b32 s1, 0x34000
	s_nop 0
	v_addc_co_u32_e32 v7, vcc, 0, v3, vcc
	v_add_co_u32_e32 v8, vcc, s1, v2
	s_mov_b32 s1, 0x38000
	s_nop 0
	v_addc_co_u32_e32 v9, vcc, 0, v3, vcc
	global_load_dwordx4 v[118:121], v[6:7], off sc0 nt
	global_load_dwordx4 v[122:125], v[8:9], off sc0 nt
	v_add_co_u32_e32 v6, vcc, s1, v2
	s_mov_b32 s1, 0x3c000
	s_nop 0
	v_addc_co_u32_e32 v7, vcc, 0, v3, vcc
	v_add_co_u32_e32 v8, vcc, s1, v2
	s_mov_b32 s1, 0x400000
	s_nop 0
	v_addc_co_u32_e32 v9, vcc, 0, v3, vcc
	v_add_co_u32_e32 v14, vcc, s1, v2
	s_mov_b32 s1, 0x404000
	s_nop 0
	v_addc_co_u32_e32 v15, vcc, 0, v3, vcc
	v_add_co_u32_e32 v16, vcc, s1, v2
	s_mov_b32 s1, 0x408000
	s_nop 0
	v_addc_co_u32_e32 v17, vcc, 0, v3, vcc
	v_add_co_u32_e32 v22, vcc, s1, v2
	s_mov_b32 s1, 0x40c000
	s_nop 0
	v_addc_co_u32_e32 v23, vcc, 0, v3, vcc
	v_add_co_u32_e32 v24, vcc, s1, v2
	s_mov_b32 s1, 0x410000
	s_nop 0
	v_addc_co_u32_e32 v25, vcc, 0, v3, vcc
	v_add_co_u32_e32 v30, vcc, s1, v2
	s_mov_b32 s1, 0x414000
	s_nop 0
	v_addc_co_u32_e32 v31, vcc, 0, v3, vcc
	v_add_co_u32_e32 v32, vcc, s1, v2
	s_mov_b32 s1, 0x418000
	s_nop 0
	v_addc_co_u32_e32 v33, vcc, 0, v3, vcc
	s_waitcnt vmcnt(0)
	v_add_co_u32_e32 v46, vcc, s1, v2
	s_mov_b32 s1, 0x41c000
	s_nop 0
	v_addc_co_u32_e32 v47, vcc, 0, v3, vcc
	v_add_co_u32_e32 v48, vcc, s1, v2
	s_mov_b32 s1, 0x420000
	s_nop 0
	v_addc_co_u32_e32 v49, vcc, 0, v3, vcc
	v_add_co_u32_e32 v62, vcc, s1, v2
	s_mov_b32 s1, 0x424000
	s_nop 0
	v_addc_co_u32_e32 v63, vcc, 0, v3, vcc
	v_add_co_u32_e32 v64, vcc, s1, v2
	s_mov_b32 s1, 0x428000
	s_nop 0
	v_addc_co_u32_e32 v65, vcc, 0, v3, vcc
	v_add_co_u32_e32 v78, vcc, s1, v2
	s_mov_b32 s1, 0x42c000
	s_nop 0
	v_addc_co_u32_e32 v79, vcc, 0, v3, vcc
	v_add_co_u32_e32 v80, vcc, s1, v2
	s_mov_b32 s1, 0x430000
	s_nop 0
	v_addc_co_u32_e32 v81, vcc, 0, v3, vcc
	global_load_dwordx4 v[130:133], v[6:7], off sc0 nt
	global_load_dwordx4 v[126:129], v[8:9], off sc0 nt
	s_nop 0
	global_load_dwordx4 v[6:9], v[14:15], off sc0 nt
	global_load_dwordx4 v[10:13], v[16:17], off sc0 nt
	global_load_dwordx4 v[18:21], v[22:23], off sc0 nt
	s_nop 0
	global_load_dwordx4 v[14:17], v[24:25], off sc0 nt
	s_nop 0
	global_load_dwordx4 v[22:25], v[30:31], off sc0 nt
	global_load_dwordx4 v[26:29], v[32:33], off sc0 nt
	global_load_dwordx4 v[42:45], v[46:47], off sc0 nt
	s_nop 0
	global_load_dwordx4 v[30:33], v[48:49], off sc0 nt
	s_nop 0
	global_load_dwordx4 v[46:49], v[62:63], off sc0 nt
	global_load_dwordx4 v[54:57], v[64:65], off sc0 nt
	global_load_dwordx4 v[74:77], v[78:79], off sc0 nt
	s_nop 0
	global_load_dwordx4 v[62:65], v[80:81], off sc0 nt
	v_add_co_u32_e32 v78, vcc, s1, v2
	s_mov_b32 s1, 0x434000
	s_nop 0
	v_addc_co_u32_e32 v79, vcc, 0, v3, vcc
	v_add_co_u32_e32 v86, vcc, s1, v2
	s_mov_b32 s1, 0x438000
	s_nop 0
	v_addc_co_u32_e32 v87, vcc, 0, v3, vcc
	v_add_co_u32_e32 v90, vcc, s1, v2
	s_mov_b32 s1, 0x43c000
	s_nop 0
	v_addc_co_u32_e32 v91, vcc, 0, v3, vcc
	v_add_co_u32_e32 v92, vcc, s1, v2
	global_load_dwordx4 v[78:81], v[78:79], off sc0 nt
	s_nop 0
	global_load_dwordx4 v[86:89], v[86:87], off sc0 nt
	v_addc_co_u32_e32 v93, vcc, 0, v3, vcc
	global_load_dwordx4 v[106:109], v[90:91], off sc0 nt
	s_nop 0
	global_load_dwordx4 v[90:93], v[92:93], off sc0 nt
	v_readlane_b32 s13, v254, 5
	v_readlane_b32 s16, v254, 8
	v_readlane_b32 s17, v254, 9
	v_readlane_b32 s18, v254, 10
	v_readlane_b32 s19, v254, 11
	s_add_i32 s2, s0, 0
	v_mul_f32_e32 v4, 0x43800000, v34
	v_mul_f32_e32 v34, 0x43800000, v38
	s_mov_b32 s0, 0xc3e00000
	v_mov_b32_e32 v1, 0x43e00000
	v_med3_f32 v4, v4, s0, v1
	v_med3_f32 v34, v34, s0, v1
	v_mov_b32_e32 v136, v5
	v_cvt_pk_fp8_f32 v136, v4, v34
	v_mul_f32_e32 v38, 0x43800000, v58
	v_mul_f32_e32 v4, 0x43800000, v50
	v_med3_f32 v34, v38, s0, v1
	v_med3_f32 v4, v4, s0, v1
	v_cvt_pk_fp8_f32 v136, v34, v4 op_sel:[0,0,1]
	v_mul_f32_e32 v4, 0x43800000, v66
	v_mul_f32_e32 v34, 0x43800000, v70
	v_med3_f32 v4, v4, s0, v1
	v_med3_f32 v34, v34, s0, v1
	v_mov_b32_e32 v137, v5
	v_cvt_pk_fp8_f32 v137, v4, v34
	v_mul_f32_e32 v38, 0x43800000, v94
	v_mul_f32_e32 v4, 0x43800000, v82
	v_med3_f32 v34, v38, s0, v1
	v_med3_f32 v4, v4, s0, v1
	v_cvt_pk_fp8_f32 v137, v34, v4 op_sel:[0,0,1]
	v_mul_f32_e32 v4, 0x43800000, v98
	v_mul_f32_e32 v34, 0x43800000, v102
	v_med3_f32 v4, v4, s0, v1
	v_med3_f32 v34, v34, s0, v1
	v_mov_b32_e32 v138, v5
	v_cvt_pk_fp8_f32 v138, v4, v34
	v_mul_f32_e32 v38, 0x43800000, v114
	v_mul_f32_e32 v4, 0x43800000, v110
	v_med3_f32 v34, v38, s0, v1
	v_med3_f32 v4, v4, s0, v1
	v_cvt_pk_fp8_f32 v138, v34, v4 op_sel:[0,0,1]
	v_mul_f32_e32 v4, 0x43800000, v118
	v_mul_f32_e32 v34, 0x43800000, v122
	v_med3_f32 v4, v4, s0, v1
	v_med3_f32 v34, v34, s0, v1
	v_mov_b32_e32 v139, v5
	v_cvt_pk_fp8_f32 v139, v4, v34
	s_waitcnt vmcnt(17)
	v_mul_f32_e32 v38, 0x43800000, v130
	s_waitcnt vmcnt(16)
	v_mul_f32_e32 v4, 0x43800000, v126
	v_med3_f32 v34, v38, s0, v1
	v_med3_f32 v4, v4, s0, v1
	v_cvt_pk_fp8_f32 v139, v34, v4 op_sel:[0,0,1]
	v_mul_u32_u24_e32 v4, 0x110, v140
	v_add3_u32 v166, s2, v135, v4
	v_mul_f32_e32 v4, 0x43800000, v35
	v_mul_f32_e32 v34, 0x43800000, v39
	v_med3_f32 v4, v4, s0, v1
	v_med3_f32 v34, v34, s0, v1
	v_mov_b32_e32 v140, v5
	v_cvt_pk_fp8_f32 v140, v4, v34
	v_mul_f32_e32 v35, 0x43800000, v59
	v_mul_f32_e32 v4, 0x43800000, v51
	v_med3_f32 v34, v35, s0, v1
	v_med3_f32 v4, v4, s0, v1
	v_cvt_pk_fp8_f32 v140, v34, v4 op_sel:[0,0,1]
	v_mul_f32_e32 v4, 0x43800000, v67
	v_mul_f32_e32 v34, 0x43800000, v71
	v_med3_f32 v4, v4, s0, v1
	v_med3_f32 v34, v34, s0, v1
	v_mov_b32_e32 v141, v5
	v_cvt_pk_fp8_f32 v141, v4, v34
	v_mul_f32_e32 v35, 0x43800000, v95
	v_mul_f32_e32 v4, 0x43800000, v83
	v_med3_f32 v34, v35, s0, v1
	v_med3_f32 v4, v4, s0, v1
	v_cvt_pk_fp8_f32 v141, v34, v4 op_sel:[0,0,1]
	v_mul_f32_e32 v4, 0x43800000, v99
	v_mul_f32_e32 v34, 0x43800000, v103
	v_med3_f32 v4, v4, s0, v1
	v_med3_f32 v34, v34, s0, v1
	v_mov_b32_e32 v142, v5
	v_cvt_pk_fp8_f32 v142, v4, v34
	v_mul_f32_e32 v35, 0x43800000, v115
	v_mul_f32_e32 v4, 0x43800000, v111
	v_med3_f32 v34, v35, s0, v1
	v_med3_f32 v4, v4, s0, v1
	v_cvt_pk_fp8_f32 v142, v34, v4 op_sel:[0,0,1]
	v_mul_f32_e32 v4, 0x43800000, v119
	v_mul_f32_e32 v34, 0x43800000, v123
	v_med3_f32 v4, v4, s0, v1
	v_med3_f32 v34, v34, s0, v1
	v_mov_b32_e32 v143, v5
	v_cvt_pk_fp8_f32 v143, v4, v34
	v_mul_f32_e32 v35, 0x43800000, v131
	v_mul_f32_e32 v4, 0x43800000, v127
	v_med3_f32 v34, v35, s0, v1
	v_med3_f32 v4, v4, s0, v1
	v_cvt_pk_fp8_f32 v143, v34, v4 op_sel:[0,0,1]
	v_mul_f32_e32 v4, 0x43800000, v36
	v_mul_f32_e32 v34, 0x43800000, v40
	v_med3_f32 v4, v4, s0, v1
	v_med3_f32 v34, v34, s0, v1
	v_mov_b32_e32 v144, v5
	v_cvt_pk_fp8_f32 v144, v4, v34
	v_mul_f32_e32 v35, 0x43800000, v60
	v_mul_f32_e32 v4, 0x43800000, v52
	v_med3_f32 v34, v35, s0, v1
	v_med3_f32 v4, v4, s0, v1
	v_cvt_pk_fp8_f32 v144, v34, v4 op_sel:[0,0,1]
	v_mul_f32_e32 v4, 0x43800000, v68
	v_mul_f32_e32 v34, 0x43800000, v72
	v_med3_f32 v4, v4, s0, v1
	v_med3_f32 v34, v34, s0, v1
	v_mov_b32_e32 v145, v5
	v_cvt_pk_fp8_f32 v145, v4, v34
	v_mul_f32_e32 v35, 0x43800000, v96
	v_mul_f32_e32 v4, 0x43800000, v84
	v_med3_f32 v34, v35, s0, v1
	v_med3_f32 v4, v4, s0, v1
	v_cvt_pk_fp8_f32 v145, v34, v4 op_sel:[0,0,1]
	v_mul_f32_e32 v4, 0x43800000, v100
	v_mul_f32_e32 v34, 0x43800000, v104
	v_med3_f32 v4, v4, s0, v1
	v_med3_f32 v34, v34, s0, v1
	v_mov_b32_e32 v146, v5
	v_cvt_pk_fp8_f32 v146, v4, v34
	v_mul_f32_e32 v35, 0x43800000, v116
	v_mul_f32_e32 v4, 0x43800000, v112
	v_med3_f32 v34, v35, s0, v1
	v_med3_f32 v4, v4, s0, v1
	v_cvt_pk_fp8_f32 v146, v34, v4 op_sel:[0,0,1]
	v_mul_f32_e32 v4, 0x43800000, v120
	v_mul_f32_e32 v34, 0x43800000, v124
	v_med3_f32 v4, v4, s0, v1
	v_med3_f32 v34, v34, s0, v1
	v_mov_b32_e32 v147, v5
	v_cvt_pk_fp8_f32 v147, v4, v34
	v_mul_f32_e32 v35, 0x43800000, v132
	v_mul_f32_e32 v4, 0x43800000, v128
	v_med3_f32 v34, v35, s0, v1
	v_med3_f32 v4, v4, s0, v1
	v_cvt_pk_fp8_f32 v147, v34, v4 op_sel:[0,0,1]
	v_mul_f32_e32 v4, 0x43800000, v37
	v_mul_f32_e32 v34, 0x43800000, v41
	v_med3_f32 v4, v4, s0, v1
	v_med3_f32 v36, v34, s0, v1
	v_mov_b32_e32 v34, v5
	v_cvt_pk_fp8_f32 v34, v4, v36
	v_mul_f32_e32 v35, 0x43800000, v61
	v_mul_f32_e32 v4, 0x43800000, v53
	v_med3_f32 v35, v35, s0, v1
	v_med3_f32 v4, v4, s0, v1
	v_cvt_pk_fp8_f32 v34, v35, v4 op_sel:[0,0,1]
	v_mul_f32_e32 v4, 0x43800000, v69
	v_mul_f32_e32 v35, 0x43800000, v73
	v_med3_f32 v4, v4, s0, v1
	v_med3_f32 v37, v35, s0, v1
	v_mov_b32_e32 v35, v5
	v_cvt_pk_fp8_f32 v35, v4, v37
	v_mul_f32_e32 v36, 0x43800000, v97
	v_mul_f32_e32 v4, 0x43800000, v85
	v_med3_f32 v36, v36, s0, v1
	v_med3_f32 v4, v4, s0, v1
	v_cvt_pk_fp8_f32 v35, v36, v4 op_sel:[0,0,1]
	v_mul_f32_e32 v4, 0x43800000, v101
	v_mul_f32_e32 v36, 0x43800000, v105
	v_med3_f32 v4, v4, s0, v1
	v_med3_f32 v38, v36, s0, v1
	v_mov_b32_e32 v36, v5
	v_cvt_pk_fp8_f32 v36, v4, v38
	v_mul_f32_e32 v37, 0x43800000, v117
	v_mul_f32_e32 v4, 0x43800000, v113
	v_med3_f32 v37, v37, s0, v1
	v_med3_f32 v4, v4, s0, v1
	v_cvt_pk_fp8_f32 v36, v37, v4 op_sel:[0,0,1]
	v_mul_f32_e32 v4, 0x43800000, v121
	v_mul_f32_e32 v37, 0x43800000, v125
	v_med3_f32 v4, v4, s0, v1
	v_med3_f32 v39, v37, s0, v1
	v_mov_b32_e32 v37, v5
	v_cvt_pk_fp8_f32 v37, v4, v39
	v_mul_f32_e32 v38, 0x43800000, v133
	v_mul_f32_e32 v4, 0x43800000, v129
	v_med3_f32 v38, v38, s0, v1
	v_med3_f32 v4, v4, s0, v1
	v_cvt_pk_fp8_f32 v37, v38, v4 op_sel:[0,0,1]
	ds_write_b128 v166, v[136:139]
	ds_write_b128 v166, v[140:143] offset:272
	ds_write_b128 v166, v[144:147] offset:544
	ds_write_b128 v166, v[34:37] offset:816
	v_add_u32_e32 v34, 0x200, v134
	v_ashrrev_i32_e32 v140, 4, v34
	v_add_u32_e32 v34, 0x400, v134
	v_ashrrev_i32_e32 v144, 4, v34
	v_add_u32_e32 v34, 0x600, v134
	v_ashrrev_i32_e32 v136, 4, v134
	v_ashrrev_i32_e32 v148, 4, v34
	v_lshlrev_b32_e32 v4, 4, v134
	v_ashrrev_i32_e32 v137, 31, v136
	v_ashrrev_i32_e32 v141, 31, v140
	v_ashrrev_i32_e32 v145, 31, v144
	v_ashrrev_i32_e32 v149, 31, v148
	s_movk_i32 s1, 0x110
	s_waitcnt lgkmcnt(0)
	s_barrier
	v_and_b32_e32 v4, 0xf0, v4
	v_lshlrev_b64 v[138:139], 11, v[136:137]
	v_lshlrev_b64 v[142:143], 11, v[140:141]
	v_lshlrev_b64 v[146:147], 11, v[144:145]
	v_lshlrev_b64 v[164:165], 11, v[148:149]
	s_mov_b32 s2, 0x800000
	v_add_co_u32_e32 v34, vcc, s2, v2
	s_mov_b32 s2, 0x804000
	s_nop 0
	v_addc_co_u32_e32 v35, vcc, 0, v3, vcc
	v_add_co_u32_e32 v38, vcc, s2, v2
	s_mov_b32 s2, 0x808000
	s_nop 0
	v_addc_co_u32_e32 v39, vcc, 0, v3, vcc
	v_add_co_u32_e32 v66, vcc, s2, v2
	s_mov_b32 s2, 0x80c000
	s_nop 0
	v_addc_co_u32_e32 v67, vcc, 0, v3, vcc
	v_add_co_u32_e32 v68, vcc, s2, v2
	s_mov_b32 s2, 0x810000
	s_nop 0
	v_addc_co_u32_e32 v69, vcc, 0, v3, vcc
	v_add_co_u32_e32 v82, vcc, s2, v2
	s_mov_b32 s2, 0x814000
	s_nop 0
	v_addc_co_u32_e32 v83, vcc, 0, v3, vcc
	v_add_co_u32_e32 v84, vcc, s2, v2
	s_mov_b32 s2, 0x818000
	s_nop 0
	v_addc_co_u32_e32 v85, vcc, 0, v3, vcc
	v_add_co_u32_e32 v98, vcc, s2, v2
	s_mov_b32 s2, 0x81c000
	s_nop 0
	v_addc_co_u32_e32 v99, vcc, 0, v3, vcc
	v_add_co_u32_e32 v100, vcc, s2, v2
	s_mov_b32 s2, 0x820000
	s_nop 0
	v_addc_co_u32_e32 v101, vcc, 0, v3, vcc
	v_add_co_u32_e32 v110, vcc, s2, v2
	s_mov_b32 s2, 0x824000
	s_nop 0
	v_addc_co_u32_e32 v111, vcc, 0, v3, vcc
	v_add_co_u32_e32 v112, vcc, s2, v2
	s_mov_b32 s2, 0x828000
	s_nop 0
	v_addc_co_u32_e32 v113, vcc, 0, v3, vcc
	global_load_dwordx4 v[34:37], v[34:35], off sc0 nt
	s_nop 0
	global_load_dwordx4 v[38:41], v[38:39], off sc0 nt
	s_nop 0
	global_load_dwordx4 v[58:61], v[66:67], off sc0 nt
	global_load_dwordx4 v[50:53], v[68:69], off sc0 nt
	s_nop 0
	global_load_dwordx4 v[66:69], v[82:83], off sc0 nt
	global_load_dwordx4 v[70:73], v[84:85], off sc0 nt
	global_load_dwordx4 v[94:97], v[98:99], off sc0 nt
	s_nop 0
	global_load_dwordx4 v[82:85], v[100:101], off sc0 nt
	s_nop 0
	global_load_dwordx4 v[98:101], v[110:111], off sc0 nt
	global_load_dwordx4 v[102:105], v[112:113], off sc0 nt
	v_add_co_u32_e32 v110, vcc, s2, v2
	s_mov_b32 s2, 0x82c000
	s_nop 0
	v_addc_co_u32_e32 v111, vcc, 0, v3, vcc
	v_add_co_u32_e32 v112, vcc, s2, v2
	s_mov_b32 s2, 0x830000
	s_nop 0
	v_addc_co_u32_e32 v113, vcc, 0, v3, vcc
	v_add_co_u32_e32 v118, vcc, s2, v2
	s_mov_b32 s2, 0x834000
	s_nop 0
	v_addc_co_u32_e32 v119, vcc, 0, v3, vcc
	v_add_co_u32_e32 v122, vcc, s2, v2
	s_mov_b32 s2, 0x838000
	s_nop 0
	v_addc_co_u32_e32 v123, vcc, 0, v3, vcc
	v_add_co_u32_e32 v126, vcc, s2, v2
	s_mov_b32 s2, 0x83c000
	s_nop 0
	v_addc_co_u32_e32 v127, vcc, 0, v3, vcc
	v_add_co_u32_e32 v128, vcc, s2, v2
	global_load_dwordx4 v[114:117], v[110:111], off sc0 nt
	s_nop 0
	global_load_dwordx4 v[110:113], v[112:113], off sc0 nt
	v_addc_co_u32_e32 v129, vcc, 0, v3, vcc
	global_load_dwordx4 v[118:121], v[118:119], off sc0 nt
	s_nop 0
	global_load_dwordx4 v[122:125], v[122:123], off sc0 nt
	s_nop 0
	global_load_dwordx4 v[130:133], v[126:127], off sc0 nt
	s_nop 0
	global_load_dwordx4 v[126:129], v[128:129], off sc0 nt
	v_add_u32_e32 v160, 0, v4
	v_lshl_add_u64 v[134:135], s[6:7], 0, v[4:5]
	s_mov_b64 s[2:3], 0x40000000
	v_lshl_add_u64 v[168:169], v[134:135], 0, s[2:3]
	v_mad_u64_u32 v[154:155], s[2:3], v136, s1, v[160:161]
	ds_read_b128 v[134:137], v154
	v_lshl_add_u64 v[150:151], v[168:169], 0, v[138:139]
	v_mad_u64_u32 v[156:157], s[2:3], v140, s1, v[160:161]
	v_mad_u64_u32 v[158:159], s[2:3], v144, s1, v[160:161]
	v_mad_u64_u32 v[162:163], s[2:3], v148, s1, v[160:161]
	ds_read_b128 v[138:141], v156
	s_waitcnt lgkmcnt(1)
	global_store_dwordx4 v[150:151], v[134:137], off nt
	v_lshl_add_u64 v[152:153], v[168:169], 0, v[142:143]
	ds_read_b128 v[134:137], v158
	ds_read_b128 v[142:145], v162
	v_lshl_add_u64 v[160:161], v[168:169], 0, v[146:147]
	v_lshl_add_u64 v[164:165], v[168:169], 0, v[164:165]
	s_waitcnt lgkmcnt(2)
	global_store_dwordx4 v[152:153], v[138:141], off nt
	s_waitcnt lgkmcnt(1)
	global_store_dwordx4 v[160:161], v[134:137], off nt
	s_waitcnt lgkmcnt(0)
	global_store_dwordx4 v[164:165], v[142:145], off nt
	s_waitcnt vmcnt(35)
	v_mul_f32_e32 v4, 0x43800000, v6
	s_waitcnt vmcnt(34)
	v_mul_f32_e32 v6, 0x43800000, v10
	v_med3_f32 v4, v4, s0, v1
	v_med3_f32 v6, v6, s0, v1
	v_mov_b32_e32 v134, v5
	v_cvt_pk_fp8_f32 v134, v4, v6
	s_waitcnt vmcnt(33)
	v_mul_f32_e32 v10, 0x43800000, v18
	s_waitcnt vmcnt(32)
	v_mul_f32_e32 v4, 0x43800000, v14
	v_med3_f32 v6, v10, s0, v1
	v_med3_f32 v4, v4, s0, v1
	v_cvt_pk_fp8_f32 v134, v6, v4 op_sel:[0,0,1]
	s_waitcnt vmcnt(31)
	v_mul_f32_e32 v4, 0x43800000, v22
	s_waitcnt vmcnt(30)
	v_mul_f32_e32 v6, 0x43800000, v26
	v_med3_f32 v4, v4, s0, v1
	v_med3_f32 v6, v6, s0, v1
	v_mov_b32_e32 v135, v5
	v_cvt_pk_fp8_f32 v135, v4, v6
	s_waitcnt vmcnt(29)
	v_mul_f32_e32 v10, 0x43800000, v42
	s_waitcnt vmcnt(28)
	v_mul_f32_e32 v4, 0x43800000, v30
	v_med3_f32 v6, v10, s0, v1
	v_med3_f32 v4, v4, s0, v1
	v_cvt_pk_fp8_f32 v135, v6, v4 op_sel:[0,0,1]
	s_waitcnt vmcnt(27)
	v_mul_f32_e32 v4, 0x43800000, v46
	s_waitcnt vmcnt(26)
	v_mul_f32_e32 v6, 0x43800000, v54
	v_med3_f32 v4, v4, s0, v1
	v_med3_f32 v6, v6, s0, v1
	v_mov_b32_e32 v136, v5
	v_cvt_pk_fp8_f32 v136, v4, v6
	s_waitcnt vmcnt(25)
	v_mul_f32_e32 v10, 0x43800000, v74
	s_waitcnt vmcnt(24)
	v_mul_f32_e32 v4, 0x43800000, v62
	v_med3_f32 v6, v10, s0, v1
	v_med3_f32 v4, v4, s0, v1
	v_cvt_pk_fp8_f32 v136, v6, v4 op_sel:[0,0,1]
	s_waitcnt vmcnt(23)
	v_mul_f32_e32 v4, 0x43800000, v78
	s_waitcnt vmcnt(22)
	v_mul_f32_e32 v6, 0x43800000, v86
	v_med3_f32 v4, v4, s0, v1
	v_med3_f32 v6, v6, s0, v1
	v_mov_b32_e32 v137, v5
	v_cvt_pk_fp8_f32 v137, v4, v6
	s_waitcnt vmcnt(21)
	v_mul_f32_e32 v10, 0x43800000, v106
	s_waitcnt vmcnt(20)
	v_mul_f32_e32 v4, 0x43800000, v90
	v_med3_f32 v6, v10, s0, v1
	v_med3_f32 v4, v4, s0, v1
	v_cvt_pk_fp8_f32 v137, v6, v4 op_sel:[0,0,1]
	v_mul_f32_e32 v4, 0x43800000, v7
	v_mul_f32_e32 v6, 0x43800000, v11
	v_med3_f32 v4, v4, s0, v1
	v_med3_f32 v6, v6, s0, v1
	v_mov_b32_e32 v138, v5
	v_cvt_pk_fp8_f32 v138, v4, v6
	v_mul_f32_e32 v7, 0x43800000, v19
	v_mul_f32_e32 v4, 0x43800000, v15
	v_med3_f32 v6, v7, s0, v1
	v_med3_f32 v4, v4, s0, v1
	v_cvt_pk_fp8_f32 v138, v6, v4 op_sel:[0,0,1]
	v_mul_f32_e32 v4, 0x43800000, v23
	v_mul_f32_e32 v6, 0x43800000, v27
	v_med3_f32 v4, v4, s0, v1
	v_med3_f32 v6, v6, s0, v1
	v_mov_b32_e32 v139, v5
	v_cvt_pk_fp8_f32 v139, v4, v6
	v_mul_f32_e32 v7, 0x43800000, v43
	v_mul_f32_e32 v4, 0x43800000, v31
	v_med3_f32 v6, v7, s0, v1
	v_med3_f32 v4, v4, s0, v1
	v_cvt_pk_fp8_f32 v139, v6, v4 op_sel:[0,0,1]
	v_mul_f32_e32 v4, 0x43800000, v47
	v_mul_f32_e32 v6, 0x43800000, v55
	v_med3_f32 v4, v4, s0, v1
	v_med3_f32 v6, v6, s0, v1
	v_mov_b32_e32 v140, v5
	v_cvt_pk_fp8_f32 v140, v4, v6
	v_mul_f32_e32 v7, 0x43800000, v75
	v_mul_f32_e32 v4, 0x43800000, v63
	v_med3_f32 v6, v7, s0, v1
	v_med3_f32 v4, v4, s0, v1
	v_cvt_pk_fp8_f32 v140, v6, v4 op_sel:[0,0,1]
	v_mul_f32_e32 v4, 0x43800000, v79
	v_mul_f32_e32 v6, 0x43800000, v87
	v_med3_f32 v4, v4, s0, v1
	v_med3_f32 v6, v6, s0, v1
	v_mov_b32_e32 v141, v5
	v_cvt_pk_fp8_f32 v141, v4, v6
	v_mul_f32_e32 v7, 0x43800000, v107
	v_mul_f32_e32 v4, 0x43800000, v91
	v_med3_f32 v6, v7, s0, v1
	v_med3_f32 v4, v4, s0, v1
	v_cvt_pk_fp8_f32 v141, v6, v4 op_sel:[0,0,1]
	v_mul_f32_e32 v4, 0x43800000, v8
	v_mul_f32_e32 v6, 0x43800000, v12
	v_med3_f32 v4, v4, s0, v1
	v_med3_f32 v6, v6, s0, v1
	v_mov_b32_e32 v142, v5
	v_cvt_pk_fp8_f32 v142, v4, v6
	v_mul_f32_e32 v7, 0x43800000, v20
	v_mul_f32_e32 v4, 0x43800000, v16
	v_med3_f32 v6, v7, s0, v1
	v_med3_f32 v4, v4, s0, v1
	v_cvt_pk_fp8_f32 v142, v6, v4 op_sel:[0,0,1]
	v_mul_f32_e32 v4, 0x43800000, v24
	v_mul_f32_e32 v6, 0x43800000, v28
	v_med3_f32 v4, v4, s0, v1
	v_med3_f32 v6, v6, s0, v1
	v_mov_b32_e32 v143, v5
	v_cvt_pk_fp8_f32 v143, v4, v6
	v_mul_f32_e32 v7, 0x43800000, v44
	v_mul_f32_e32 v4, 0x43800000, v32
	v_med3_f32 v6, v7, s0, v1
	v_med3_f32 v4, v4, s0, v1
	v_cvt_pk_fp8_f32 v143, v6, v4 op_sel:[0,0,1]
	v_mul_f32_e32 v4, 0x43800000, v48
	v_mul_f32_e32 v6, 0x43800000, v56
	v_med3_f32 v4, v4, s0, v1
	v_med3_f32 v6, v6, s0, v1
	v_mov_b32_e32 v144, v5
	v_cvt_pk_fp8_f32 v144, v4, v6
	v_mul_f32_e32 v7, 0x43800000, v76
	v_mul_f32_e32 v4, 0x43800000, v64
	v_med3_f32 v6, v7, s0, v1
	v_med3_f32 v4, v4, s0, v1
	v_cvt_pk_fp8_f32 v144, v6, v4 op_sel:[0,0,1]
	v_mul_f32_e32 v4, 0x43800000, v80
	v_mul_f32_e32 v6, 0x43800000, v88
	v_med3_f32 v4, v4, s0, v1
	v_med3_f32 v6, v6, s0, v1
	v_mov_b32_e32 v145, v5
	v_cvt_pk_fp8_f32 v145, v4, v6
	v_mul_f32_e32 v7, 0x43800000, v108
	v_mul_f32_e32 v4, 0x43800000, v92
	v_med3_f32 v6, v7, s0, v1
	v_med3_f32 v4, v4, s0, v1
	v_cvt_pk_fp8_f32 v145, v6, v4 op_sel:[0,0,1]
	v_mul_f32_e32 v4, 0x43800000, v9
	v_mul_f32_e32 v6, 0x43800000, v13
	v_med3_f32 v4, v4, s0, v1
	v_med3_f32 v8, v6, s0, v1
	v_mov_b32_e32 v6, v5
	v_cvt_pk_fp8_f32 v6, v4, v8
	v_mul_f32_e32 v7, 0x43800000, v21
	v_mul_f32_e32 v4, 0x43800000, v17
	v_med3_f32 v7, v7, s0, v1
	v_med3_f32 v4, v4, s0, v1
	v_cvt_pk_fp8_f32 v6, v7, v4 op_sel:[0,0,1]
	v_mul_f32_e32 v4, 0x43800000, v25
	v_mul_f32_e32 v7, 0x43800000, v29
	v_med3_f32 v4, v4, s0, v1
	v_med3_f32 v9, v7, s0, v1
	v_mov_b32_e32 v7, v5
	v_cvt_pk_fp8_f32 v7, v4, v9
	v_mul_f32_e32 v8, 0x43800000, v45
	v_mul_f32_e32 v4, 0x43800000, v33
	v_med3_f32 v8, v8, s0, v1
	v_med3_f32 v4, v4, s0, v1
	v_cvt_pk_fp8_f32 v7, v8, v4 op_sel:[0,0,1]
	v_mul_f32_e32 v4, 0x43800000, v49
	v_mul_f32_e32 v8, 0x43800000, v57
	v_med3_f32 v4, v4, s0, v1
	v_med3_f32 v10, v8, s0, v1
	v_mov_b32_e32 v8, v5
	v_cvt_pk_fp8_f32 v8, v4, v10
	v_mul_f32_e32 v9, 0x43800000, v77
	v_mul_f32_e32 v4, 0x43800000, v65
	v_med3_f32 v9, v9, s0, v1
	v_med3_f32 v4, v4, s0, v1
	v_cvt_pk_fp8_f32 v8, v9, v4 op_sel:[0,0,1]
	v_mul_f32_e32 v4, 0x43800000, v81
	v_mul_f32_e32 v9, 0x43800000, v89
	v_med3_f32 v4, v4, s0, v1
	v_med3_f32 v11, v9, s0, v1
	v_mov_b32_e32 v9, v5
	v_cvt_pk_fp8_f32 v9, v4, v11
	v_mul_f32_e32 v10, 0x43800000, v109
	v_mul_f32_e32 v4, 0x43800000, v93
	v_med3_f32 v10, v10, s0, v1
	v_med3_f32 v4, v4, s0, v1
	v_cvt_pk_fp8_f32 v9, v10, v4 op_sel:[0,0,1]
	ds_write_b128 v166, v[134:137] offset:34816
	ds_write_b128 v166, v[138:141] offset:35088
	ds_write_b128 v166, v[142:145] offset:35360
	ds_write_b128 v166, v[6:9] offset:35632
	s_waitcnt lgkmcnt(0)
	s_barrier
	s_mov_b32 s1, 0xc00000
	v_add_co_u32_e32 v6, vcc, s1, v2
	s_mov_b32 s1, 0xc04000
	s_nop 0
	v_addc_co_u32_e32 v7, vcc, 0, v3, vcc
	v_add_co_u32_e32 v10, vcc, s1, v2
	s_mov_b32 s1, 0xc08000
	s_nop 0
	v_addc_co_u32_e32 v11, vcc, 0, v3, vcc
	global_load_dwordx4 v[6:9], v[6:7], off sc0 nt
	s_nop 0
	global_load_dwordx4 v[14:17], v[10:11], off sc0 nt
	v_add_co_u32_e32 v10, vcc, s1, v2
	s_mov_b32 s1, 0xc0c000
	s_nop 0
	v_addc_co_u32_e32 v11, vcc, 0, v3, vcc
	v_add_co_u32_e32 v12, vcc, s1, v2
	s_mov_b32 s1, 0xc10000
	s_nop 0
	v_addc_co_u32_e32 v13, vcc, 0, v3, vcc
	global_load_dwordx4 v[30:33], v[10:11], off sc0 nt
	global_load_dwordx4 v[22:25], v[12:13], off sc0 nt
	v_add_co_u32_e32 v10, vcc, s1, v2
	s_mov_b32 s1, 0xc14000
	s_nop 0
	v_addc_co_u32_e32 v11, vcc, 0, v3, vcc
	v_add_co_u32_e32 v12, vcc, s1, v2
	s_mov_b32 s1, 0xc18000
	s_nop 0
	v_addc_co_u32_e32 v13, vcc, 0, v3, vcc
	global_load_dwordx4 v[42:45], v[10:11], off sc0 nt
	global_load_dwordx4 v[46:49], v[12:13], off sc0 nt
	v_add_co_u32_e32 v10, vcc, s1, v2
	s_mov_b32 s1, 0xc1c000
	s_nop 0
	v_addc_co_u32_e32 v11, vcc, 0, v3, vcc
	v_add_co_u32_e32 v12, vcc, s1, v2
	s_mov_b32 s1, 0xc20000
	s_nop 0
	v_addc_co_u32_e32 v13, vcc, 0, v3, vcc
	global_load_dwordx4 v[62:65], v[10:11], off sc0 nt
	global_load_dwordx4 v[54:57], v[12:13], off sc0 nt
	v_add_co_u32_e32 v10, vcc, s1, v2
	s_mov_b32 s1, 0xc24000
	s_nop 0
	v_addc_co_u32_e32 v11, vcc, 0, v3, vcc
	v_add_co_u32_e32 v12, vcc, s1, v2
	s_mov_b32 s1, 0xc28000
	s_nop 0
	v_addc_co_u32_e32 v13, vcc, 0, v3, vcc
	global_load_dwordx4 v[74:77], v[10:11], off sc0 nt
	global_load_dwordx4 v[78:81], v[12:13], off sc0 nt
	v_add_co_u32_e32 v10, vcc, s1, v2
	s_mov_b32 s1, 0xc2c000
	s_nop 0
	v_addc_co_u32_e32 v11, vcc, 0, v3, vcc
	v_add_co_u32_e32 v12, vcc, s1, v2
	s_mov_b32 s1, 0xc30000
	s_nop 0
	v_addc_co_u32_e32 v13, vcc, 0, v3, vcc
	global_load_dwordx4 v[106:109], v[10:11], off sc0 nt
	global_load_dwordx4 v[86:89], v[12:13], off sc0 nt
	v_add_co_u32_e32 v10, vcc, s1, v2
	s_mov_b32 s1, 0xc34000
	s_nop 0
	v_addc_co_u32_e32 v11, vcc, 0, v3, vcc
	v_add_co_u32_e32 v12, vcc, s1, v2
	s_mov_b32 s1, 0xc38000
	s_nop 0
	v_addc_co_u32_e32 v13, vcc, 0, v3, vcc
	global_load_dwordx4 v[134:137], v[10:11], off sc0 nt
	global_load_dwordx4 v[138:141], v[12:13], off sc0 nt
	v_add_co_u32_e32 v10, vcc, s1, v2
	s_mov_b32 s1, 0xc3c000
	s_nop 0
	v_addc_co_u32_e32 v11, vcc, 0, v3, vcc
	v_add_co_u32_e32 v12, vcc, s1, v2
	s_nop 1
	v_addc_co_u32_e32 v13, vcc, 0, v3, vcc
	global_load_dwordx4 v[146:149], v[10:11], off sc0 nt
	global_load_dwordx4 v[142:145], v[12:13], off sc0 nt
	ds_read_b128 v[10:13], v154 offset:34816
	ds_read_b128 v[18:21], v156 offset:34816
	ds_read_b128 v[26:29], v158 offset:34816
	ds_read_b128 v[90:93], v162 offset:34816
	s_waitcnt lgkmcnt(3)
	global_store_dwordx4 v[150:151], v[10:13], off offset:256 nt
	s_waitcnt lgkmcnt(2)
	global_store_dwordx4 v[152:153], v[18:21], off offset:256 nt
	s_waitcnt lgkmcnt(1)
	global_store_dwordx4 v[160:161], v[26:29], off offset:256 nt
	s_waitcnt lgkmcnt(0)
	global_store_dwordx4 v[164:165], v[90:93], off offset:256 nt
	s_waitcnt vmcnt(39)
	v_mul_f32_e32 v4, 0x43800000, v34
	s_waitcnt vmcnt(38)
	v_mul_f32_e32 v10, 0x43800000, v38
	v_med3_f32 v4, v4, s0, v1
	v_med3_f32 v12, v10, s0, v1
	v_mov_b32_e32 v10, v5
	v_cvt_pk_fp8_f32 v10, v4, v12
	s_waitcnt vmcnt(37)
	v_mul_f32_e32 v11, 0x43800000, v58
	s_waitcnt vmcnt(36)
	v_mul_f32_e32 v4, 0x43800000, v50
	v_med3_f32 v11, v11, s0, v1
	v_med3_f32 v4, v4, s0, v1
	v_cvt_pk_fp8_f32 v10, v11, v4 op_sel:[0,0,1]
	s_waitcnt vmcnt(35)
	v_mul_f32_e32 v4, 0x43800000, v66
	s_waitcnt vmcnt(34)
	v_mul_f32_e32 v11, 0x43800000, v70
	v_med3_f32 v4, v4, s0, v1
	v_med3_f32 v13, v11, s0, v1
	v_mov_b32_e32 v11, v5
	v_cvt_pk_fp8_f32 v11, v4, v13
	s_waitcnt vmcnt(33)
	v_mul_f32_e32 v12, 0x43800000, v94
	s_waitcnt vmcnt(32)
	v_mul_f32_e32 v4, 0x43800000, v82
	v_med3_f32 v12, v12, s0, v1
	v_med3_f32 v4, v4, s0, v1
	v_cvt_pk_fp8_f32 v11, v12, v4 op_sel:[0,0,1]
	s_waitcnt vmcnt(31)
	v_mul_f32_e32 v4, 0x43800000, v98
	s_waitcnt vmcnt(30)
	v_mul_f32_e32 v12, 0x43800000, v102
	v_med3_f32 v4, v4, s0, v1
	v_med3_f32 v18, v12, s0, v1
	v_mov_b32_e32 v12, v5
	v_cvt_pk_fp8_f32 v12, v4, v18
	s_waitcnt vmcnt(29)
	v_mul_f32_e32 v13, 0x43800000, v114
	s_waitcnt vmcnt(28)
	v_mul_f32_e32 v4, 0x43800000, v110
	v_med3_f32 v13, v13, s0, v1
	v_med3_f32 v4, v4, s0, v1
	v_cvt_pk_fp8_f32 v12, v13, v4 op_sel:[0,0,1]
	s_waitcnt vmcnt(27)
	v_mul_f32_e32 v4, 0x43800000, v118
	s_waitcnt vmcnt(26)
	v_mul_f32_e32 v13, 0x43800000, v122
	v_med3_f32 v4, v4, s0, v1
	v_med3_f32 v19, v13, s0, v1
	v_mov_b32_e32 v13, v5
	v_cvt_pk_fp8_f32 v13, v4, v19
	s_waitcnt vmcnt(25)
	v_mul_f32_e32 v18, 0x43800000, v130
	s_waitcnt vmcnt(24)
	v_mul_f32_e32 v4, 0x43800000, v126
	v_med3_f32 v18, v18, s0, v1
	v_med3_f32 v4, v4, s0, v1
	v_cvt_pk_fp8_f32 v13, v18, v4 op_sel:[0,0,1]
	v_mul_f32_e32 v4, 0x43800000, v35
	v_mul_f32_e32 v18, 0x43800000, v39
	v_med3_f32 v4, v4, s0, v1
	v_med3_f32 v20, v18, s0, v1
	v_mov_b32_e32 v18, v5
	v_cvt_pk_fp8_f32 v18, v4, v20
	v_mul_f32_e32 v19, 0x43800000, v59
	v_mul_f32_e32 v4, 0x43800000, v51
	v_med3_f32 v19, v19, s0, v1
	v_med3_f32 v4, v4, s0, v1
	v_cvt_pk_fp8_f32 v18, v19, v4 op_sel:[0,0,1]
	v_mul_f32_e32 v4, 0x43800000, v67
	v_mul_f32_e32 v19, 0x43800000, v71
	v_med3_f32 v4, v4, s0, v1
	v_med3_f32 v21, v19, s0, v1
	v_mov_b32_e32 v19, v5
	v_cvt_pk_fp8_f32 v19, v4, v21
	v_mul_f32_e32 v20, 0x43800000, v95
	v_mul_f32_e32 v4, 0x43800000, v83
	v_med3_f32 v20, v20, s0, v1
	v_med3_f32 v4, v4, s0, v1
	v_cvt_pk_fp8_f32 v19, v20, v4 op_sel:[0,0,1]
	v_mul_f32_e32 v4, 0x43800000, v99
	v_mul_f32_e32 v20, 0x43800000, v103
	v_med3_f32 v4, v4, s0, v1
	v_med3_f32 v26, v20, s0, v1
	v_mov_b32_e32 v20, v5
	v_cvt_pk_fp8_f32 v20, v4, v26
	v_mul_f32_e32 v21, 0x43800000, v115
	v_mul_f32_e32 v4, 0x43800000, v111
	v_med3_f32 v21, v21, s0, v1
	v_med3_f32 v4, v4, s0, v1
	v_cvt_pk_fp8_f32 v20, v21, v4 op_sel:[0,0,1]
	v_mul_f32_e32 v4, 0x43800000, v119
	v_mul_f32_e32 v21, 0x43800000, v123
	v_med3_f32 v4, v4, s0, v1
	v_med3_f32 v27, v21, s0, v1
	v_mov_b32_e32 v21, v5
	v_cvt_pk_fp8_f32 v21, v4, v27
	v_mul_f32_e32 v26, 0x43800000, v131
	v_mul_f32_e32 v4, 0x43800000, v127
	v_med3_f32 v26, v26, s0, v1
	v_med3_f32 v4, v4, s0, v1
	v_cvt_pk_fp8_f32 v21, v26, v4 op_sel:[0,0,1]
	v_mul_f32_e32 v4, 0x43800000, v36
	v_mul_f32_e32 v26, 0x43800000, v40
	v_med3_f32 v4, v4, s0, v1
	v_med3_f32 v28, v26, s0, v1
	v_mov_b32_e32 v26, v5
	v_cvt_pk_fp8_f32 v26, v4, v28
	v_mul_f32_e32 v27, 0x43800000, v60
	v_mul_f32_e32 v4, 0x43800000, v52
	v_med3_f32 v27, v27, s0, v1
	v_med3_f32 v4, v4, s0, v1
	v_cvt_pk_fp8_f32 v26, v27, v4 op_sel:[0,0,1]
	v_mul_f32_e32 v4, 0x43800000, v68
	v_mul_f32_e32 v27, 0x43800000, v72
	v_med3_f32 v4, v4, s0, v1
	v_med3_f32 v29, v27, s0, v1
	v_mov_b32_e32 v27, v5
	v_cvt_pk_fp8_f32 v27, v4, v29
	v_mul_f32_e32 v28, 0x43800000, v96
	v_mul_f32_e32 v4, 0x43800000, v84
	v_med3_f32 v28, v28, s0, v1
	v_med3_f32 v4, v4, s0, v1
	v_cvt_pk_fp8_f32 v27, v28, v4 op_sel:[0,0,1]
	v_mul_f32_e32 v4, 0x43800000, v100
	v_mul_f32_e32 v28, 0x43800000, v104
	v_med3_f32 v4, v4, s0, v1
	v_med3_f32 v34, v28, s0, v1
	v_mov_b32_e32 v28, v5
	v_cvt_pk_fp8_f32 v28, v4, v34
	v_mul_f32_e32 v29, 0x43800000, v116
	v_mul_f32_e32 v4, 0x43800000, v112
	v_med3_f32 v29, v29, s0, v1
	v_med3_f32 v4, v4, s0, v1
	v_cvt_pk_fp8_f32 v28, v29, v4 op_sel:[0,0,1]
	v_mul_f32_e32 v4, 0x43800000, v120
	v_mul_f32_e32 v29, 0x43800000, v124
	v_med3_f32 v4, v4, s0, v1
	v_med3_f32 v35, v29, s0, v1
	v_mov_b32_e32 v29, v5
	v_cvt_pk_fp8_f32 v29, v4, v35
	v_mul_f32_e32 v34, 0x43800000, v132
	v_mul_f32_e32 v4, 0x43800000, v128
	v_med3_f32 v34, v34, s0, v1
	v_med3_f32 v4, v4, s0, v1
	v_cvt_pk_fp8_f32 v29, v34, v4 op_sel:[0,0,1]
	v_mul_f32_e32 v4, 0x43800000, v37
	v_mul_f32_e32 v34, 0x43800000, v41
	v_med3_f32 v4, v4, s0, v1
	v_med3_f32 v36, v34, s0, v1
	v_mov_b32_e32 v34, v5
	v_cvt_pk_fp8_f32 v34, v4, v36
	v_mul_f32_e32 v35, 0x43800000, v61
	v_mul_f32_e32 v4, 0x43800000, v53
	v_med3_f32 v35, v35, s0, v1
	v_med3_f32 v4, v4, s0, v1
	v_cvt_pk_fp8_f32 v34, v35, v4 op_sel:[0,0,1]
	v_mul_f32_e32 v4, 0x43800000, v69
	v_mul_f32_e32 v35, 0x43800000, v73
	v_med3_f32 v4, v4, s0, v1
	v_med3_f32 v37, v35, s0, v1
	v_mov_b32_e32 v35, v5
	v_cvt_pk_fp8_f32 v35, v4, v37
	v_mul_f32_e32 v36, 0x43800000, v97
	v_mul_f32_e32 v4, 0x43800000, v85
	v_med3_f32 v36, v36, s0, v1
	v_med3_f32 v4, v4, s0, v1
	v_cvt_pk_fp8_f32 v35, v36, v4 op_sel:[0,0,1]
	v_mul_f32_e32 v4, 0x43800000, v101
	v_mul_f32_e32 v36, 0x43800000, v105
	v_med3_f32 v4, v4, s0, v1
	v_med3_f32 v38, v36, s0, v1
	v_mov_b32_e32 v36, v5
	v_cvt_pk_fp8_f32 v36, v4, v38
	v_mul_f32_e32 v37, 0x43800000, v117
	v_mul_f32_e32 v4, 0x43800000, v113
	v_med3_f32 v37, v37, s0, v1
	v_med3_f32 v4, v4, s0, v1
	v_cvt_pk_fp8_f32 v36, v37, v4 op_sel:[0,0,1]
	v_mul_f32_e32 v4, 0x43800000, v121
	v_mul_f32_e32 v37, 0x43800000, v125
	v_med3_f32 v4, v4, s0, v1
	v_med3_f32 v39, v37, s0, v1
	v_mov_b32_e32 v37, v5
	v_cvt_pk_fp8_f32 v37, v4, v39
	v_mul_f32_e32 v38, 0x43800000, v133
	v_mul_f32_e32 v4, 0x43800000, v129
	v_med3_f32 v38, v38, s0, v1
	v_med3_f32 v4, v4, s0, v1
	v_cvt_pk_fp8_f32 v37, v38, v4 op_sel:[0,0,1]
	ds_write_b128 v166, v[10:13]
	ds_write_b128 v166, v[18:21] offset:272
	ds_write_b128 v166, v[26:29] offset:544
	ds_write_b128 v166, v[34:37] offset:816
	s_waitcnt lgkmcnt(0)
	s_barrier
	s_mov_b32 s1, 0x1000000
	v_add_co_u32_e32 v10, vcc, s1, v2
	s_mov_b32 s1, 0x1004000
	s_nop 0
	v_addc_co_u32_e32 v11, vcc, 0, v3, vcc
	v_add_co_u32_e32 v18, vcc, s1, v2
	s_mov_b32 s1, 0x1008000
	s_nop 0
	v_addc_co_u32_e32 v19, vcc, 0, v3, vcc
	v_add_co_u32_e32 v38, vcc, s1, v2
	s_mov_b32 s1, 0x100c000
	s_nop 0
	v_addc_co_u32_e32 v39, vcc, 0, v3, vcc
	v_add_co_u32_e32 v40, vcc, s1, v2
	s_mov_b32 s1, 0x1010000
	s_nop 0
	v_addc_co_u32_e32 v41, vcc, 0, v3, vcc
	v_add_co_u32_e32 v58, vcc, s1, v2
	s_mov_b32 s1, 0x1014000
	s_nop 0
	v_addc_co_u32_e32 v59, vcc, 0, v3, vcc
	v_add_co_u32_e32 v60, vcc, s1, v2
	s_mov_b32 s1, 0x1018000
	s_nop 0
	v_addc_co_u32_e32 v61, vcc, 0, v3, vcc
	v_add_co_u32_e32 v70, vcc, s1, v2
	s_mov_b32 s1, 0x101c000
	s_nop 0
	v_addc_co_u32_e32 v71, vcc, 0, v3, vcc
	v_add_co_u32_e32 v72, vcc, s1, v2
	s_mov_b32 s1, 0x1020000
	s_nop 0
	v_addc_co_u32_e32 v73, vcc, 0, v3, vcc
	v_add_co_u32_e32 v90, vcc, s1, v2
	s_mov_b32 s1, 0x1024000
	s_nop 0
	v_addc_co_u32_e32 v91, vcc, 0, v3, vcc
	v_add_co_u32_e32 v92, vcc, s1, v2
	s_mov_b32 s1, 0x1028000
	s_nop 0
	v_addc_co_u32_e32 v93, vcc, 0, v3, vcc
	global_load_dwordx4 v[10:13], v[10:11], off sc0 nt
	s_nop 0
	global_load_dwordx4 v[18:21], v[18:19], off sc0 nt
	s_nop 0
	global_load_dwordx4 v[34:37], v[38:39], off sc0 nt
	global_load_dwordx4 v[26:29], v[40:41], off sc0 nt
	s_nop 0
	global_load_dwordx4 v[38:41], v[58:59], off sc0 nt
	global_load_dwordx4 v[50:53], v[60:61], off sc0 nt
	global_load_dwordx4 v[66:69], v[70:71], off sc0 nt
	s_nop 0
	global_load_dwordx4 v[58:61], v[72:73], off sc0 nt
	s_nop 0
	global_load_dwordx4 v[70:73], v[90:91], off sc0 nt
	global_load_dwordx4 v[82:85], v[92:93], off sc0 nt
	v_add_co_u32_e32 v90, vcc, s1, v2
	s_mov_b32 s1, 0x102c000
	s_nop 0
	v_addc_co_u32_e32 v91, vcc, 0, v3, vcc
	v_add_co_u32_e32 v92, vcc, s1, v2
	s_mov_b32 s1, 0x1030000
	s_nop 0
	v_addc_co_u32_e32 v93, vcc, 0, v3, vcc
	v_add_co_u32_e32 v98, vcc, s1, v2
	s_mov_b32 s1, 0x1034000
	s_nop 0
	v_addc_co_u32_e32 v99, vcc, 0, v3, vcc
	v_add_co_u32_e32 v102, vcc, s1, v2
	s_mov_b32 s1, 0x1038000
	s_nop 0
	v_addc_co_u32_e32 v103, vcc, 0, v3, vcc
	global_load_dwordx4 v[94:97], v[90:91], off sc0 nt
	s_nop 0
	global_load_dwordx4 v[90:93], v[92:93], off sc0 nt
	s_nop 0
	global_load_dwordx4 v[98:101], v[98:99], off sc0 nt
	s_nop 0
	global_load_dwordx4 v[110:113], v[102:103], off sc0 nt
	v_add_co_u32_e32 v102, vcc, s1, v2
	s_mov_b32 s1, 0x103c000
	s_nop 0
	v_addc_co_u32_e32 v103, vcc, 0, v3, vcc
	v_add_co_u32_e32 v104, vcc, s1, v2
	s_nop 1
	v_addc_co_u32_e32 v105, vcc, 0, v3, vcc
	global_load_dwordx4 v[126:129], v[102:103], off sc0 nt
	global_load_dwordx4 v[118:121], v[104:105], off sc0 nt
	ds_read_b128 v[102:105], v154
	ds_read_b128 v[114:117], v156
	ds_read_b128 v[122:125], v158
	ds_read_b128 v[130:133], v162
	s_waitcnt lgkmcnt(3)
	global_store_dwordx4 v[150:151], v[102:105], off offset:512 nt
	s_waitcnt lgkmcnt(2)
	global_store_dwordx4 v[152:153], v[114:117], off offset:512 nt
	s_waitcnt lgkmcnt(1)
	global_store_dwordx4 v[160:161], v[122:125], off offset:512 nt
	s_waitcnt lgkmcnt(0)
	global_store_dwordx4 v[164:165], v[130:133], off offset:512 nt
	s_waitcnt vmcnt(39)
	v_mul_f32_e32 v4, 0x43800000, v6
	s_waitcnt vmcnt(38)
	v_mul_f32_e32 v6, 0x43800000, v14
	v_med3_f32 v4, v4, s0, v1
	v_med3_f32 v6, v6, s0, v1
	v_mov_b32_e32 v102, v5
	v_cvt_pk_fp8_f32 v102, v4, v6
	s_waitcnt vmcnt(37)
	v_mul_f32_e32 v14, 0x43800000, v30
	s_waitcnt vmcnt(36)
	v_mul_f32_e32 v4, 0x43800000, v22
	v_med3_f32 v6, v14, s0, v1
	v_med3_f32 v4, v4, s0, v1
	v_cvt_pk_fp8_f32 v102, v6, v4 op_sel:[0,0,1]
	s_waitcnt vmcnt(35)
	v_mul_f32_e32 v4, 0x43800000, v42
	s_waitcnt vmcnt(34)
	v_mul_f32_e32 v6, 0x43800000, v46
	v_med3_f32 v4, v4, s0, v1
	v_med3_f32 v6, v6, s0, v1
	v_mov_b32_e32 v103, v5
	v_cvt_pk_fp8_f32 v103, v4, v6
	s_waitcnt vmcnt(33)
	v_mul_f32_e32 v14, 0x43800000, v62
	s_waitcnt vmcnt(32)
	v_mul_f32_e32 v4, 0x43800000, v54
	v_med3_f32 v6, v14, s0, v1
	v_med3_f32 v4, v4, s0, v1
	v_cvt_pk_fp8_f32 v103, v6, v4 op_sel:[0,0,1]
	s_waitcnt vmcnt(31)
	v_mul_f32_e32 v4, 0x43800000, v74
	s_waitcnt vmcnt(30)
	v_mul_f32_e32 v6, 0x43800000, v78
	v_med3_f32 v4, v4, s0, v1
	v_med3_f32 v6, v6, s0, v1
	v_mov_b32_e32 v104, v5
	v_cvt_pk_fp8_f32 v104, v4, v6
	s_waitcnt vmcnt(29)
	v_mul_f32_e32 v14, 0x43800000, v106
	s_waitcnt vmcnt(28)
	v_mul_f32_e32 v4, 0x43800000, v86
	v_med3_f32 v6, v14, s0, v1
	v_med3_f32 v4, v4, s0, v1
	v_cvt_pk_fp8_f32 v104, v6, v4 op_sel:[0,0,1]
	s_waitcnt vmcnt(27)
	v_mul_f32_e32 v4, 0x43800000, v134
	s_waitcnt vmcnt(26)
	v_mul_f32_e32 v6, 0x43800000, v138
	v_med3_f32 v4, v4, s0, v1
	v_med3_f32 v6, v6, s0, v1
	v_mov_b32_e32 v105, v5
	v_cvt_pk_fp8_f32 v105, v4, v6
	s_waitcnt vmcnt(25)
	v_mul_f32_e32 v14, 0x43800000, v146
	s_waitcnt vmcnt(24)
	v_mul_f32_e32 v4, 0x43800000, v142
	v_med3_f32 v6, v14, s0, v1
	v_med3_f32 v4, v4, s0, v1
	v_cvt_pk_fp8_f32 v105, v6, v4 op_sel:[0,0,1]
	v_mul_f32_e32 v4, 0x43800000, v7
	v_mul_f32_e32 v6, 0x43800000, v15
	v_med3_f32 v4, v4, s0, v1
	v_med3_f32 v6, v6, s0, v1
	v_mov_b32_e32 v114, v5
	v_cvt_pk_fp8_f32 v114, v4, v6
	v_mul_f32_e32 v7, 0x43800000, v31
	v_mul_f32_e32 v4, 0x43800000, v23
	v_med3_f32 v6, v7, s0, v1
	v_med3_f32 v4, v4, s0, v1
	v_cvt_pk_fp8_f32 v114, v6, v4 op_sel:[0,0,1]
	v_mul_f32_e32 v4, 0x43800000, v43
	v_mul_f32_e32 v6, 0x43800000, v47
	v_med3_f32 v4, v4, s0, v1
	v_med3_f32 v6, v6, s0, v1
	v_mov_b32_e32 v115, v5
	v_cvt_pk_fp8_f32 v115, v4, v6
	v_mul_f32_e32 v7, 0x43800000, v63
	v_mul_f32_e32 v4, 0x43800000, v55
	v_med3_f32 v6, v7, s0, v1
	v_med3_f32 v4, v4, s0, v1
	v_cvt_pk_fp8_f32 v115, v6, v4 op_sel:[0,0,1]
	v_mul_f32_e32 v4, 0x43800000, v75
	v_mul_f32_e32 v6, 0x43800000, v79
	v_med3_f32 v4, v4, s0, v1
	v_med3_f32 v6, v6, s0, v1
	v_mov_b32_e32 v116, v5
	v_cvt_pk_fp8_f32 v116, v4, v6
	v_mul_f32_e32 v7, 0x43800000, v107
	v_mul_f32_e32 v4, 0x43800000, v87
	v_med3_f32 v6, v7, s0, v1
	v_med3_f32 v4, v4, s0, v1
	v_cvt_pk_fp8_f32 v116, v6, v4 op_sel:[0,0,1]
	v_mul_f32_e32 v4, 0x43800000, v135
	v_mul_f32_e32 v6, 0x43800000, v139
	v_med3_f32 v4, v4, s0, v1
	v_med3_f32 v6, v6, s0, v1
	v_mov_b32_e32 v117, v5
	v_cvt_pk_fp8_f32 v117, v4, v6
	v_mul_f32_e32 v7, 0x43800000, v147
	v_mul_f32_e32 v4, 0x43800000, v143
	v_med3_f32 v6, v7, s0, v1
	v_med3_f32 v4, v4, s0, v1
	v_cvt_pk_fp8_f32 v117, v6, v4 op_sel:[0,0,1]
	v_mul_f32_e32 v4, 0x43800000, v8
	v_mul_f32_e32 v6, 0x43800000, v16
	v_med3_f32 v4, v4, s0, v1
	v_med3_f32 v6, v6, s0, v1
	v_mov_b32_e32 v122, v5
	v_cvt_pk_fp8_f32 v122, v4, v6
	v_mul_f32_e32 v7, 0x43800000, v32
	v_mul_f32_e32 v4, 0x43800000, v24
	v_med3_f32 v6, v7, s0, v1
	v_med3_f32 v4, v4, s0, v1
	v_cvt_pk_fp8_f32 v122, v6, v4 op_sel:[0,0,1]
	v_mul_f32_e32 v4, 0x43800000, v44
	v_mul_f32_e32 v6, 0x43800000, v48
	v_med3_f32 v4, v4, s0, v1
	v_med3_f32 v6, v6, s0, v1
	v_mov_b32_e32 v123, v5
	v_cvt_pk_fp8_f32 v123, v4, v6
	v_mul_f32_e32 v7, 0x43800000, v64
	v_mul_f32_e32 v4, 0x43800000, v56
	v_med3_f32 v6, v7, s0, v1
	v_med3_f32 v4, v4, s0, v1
	v_cvt_pk_fp8_f32 v123, v6, v4 op_sel:[0,0,1]
	v_mul_f32_e32 v4, 0x43800000, v76
	v_mul_f32_e32 v6, 0x43800000, v80
	v_med3_f32 v4, v4, s0, v1
	v_med3_f32 v6, v6, s0, v1
	v_mov_b32_e32 v124, v5
	v_cvt_pk_fp8_f32 v124, v4, v6
	v_mul_f32_e32 v7, 0x43800000, v108
	v_mul_f32_e32 v4, 0x43800000, v88
	v_med3_f32 v6, v7, s0, v1
	v_med3_f32 v4, v4, s0, v1
	v_cvt_pk_fp8_f32 v124, v6, v4 op_sel:[0,0,1]
	v_mul_f32_e32 v4, 0x43800000, v136
	v_mul_f32_e32 v6, 0x43800000, v140
	v_med3_f32 v4, v4, s0, v1
	v_med3_f32 v6, v6, s0, v1
	v_mov_b32_e32 v125, v5
	v_cvt_pk_fp8_f32 v125, v4, v6
	v_mul_f32_e32 v7, 0x43800000, v148
	v_mul_f32_e32 v4, 0x43800000, v144
	v_med3_f32 v6, v7, s0, v1
	v_med3_f32 v4, v4, s0, v1
	v_cvt_pk_fp8_f32 v125, v6, v4 op_sel:[0,0,1]
	v_mul_f32_e32 v4, 0x43800000, v9
	v_mul_f32_e32 v6, 0x43800000, v17
	v_med3_f32 v4, v4, s0, v1
	v_med3_f32 v8, v6, s0, v1
	v_mov_b32_e32 v6, v5
	v_cvt_pk_fp8_f32 v6, v4, v8
	v_mul_f32_e32 v7, 0x43800000, v33
	v_mul_f32_e32 v4, 0x43800000, v25
	v_med3_f32 v7, v7, s0, v1
	v_med3_f32 v4, v4, s0, v1
	v_cvt_pk_fp8_f32 v6, v7, v4 op_sel:[0,0,1]
	v_mul_f32_e32 v4, 0x43800000, v45
	v_mul_f32_e32 v7, 0x43800000, v49
	v_med3_f32 v4, v4, s0, v1
	v_med3_f32 v9, v7, s0, v1
	v_mov_b32_e32 v7, v5
	v_cvt_pk_fp8_f32 v7, v4, v9
	v_mul_f32_e32 v8, 0x43800000, v65
	v_mul_f32_e32 v4, 0x43800000, v57
	v_med3_f32 v8, v8, s0, v1
	v_med3_f32 v4, v4, s0, v1
	v_cvt_pk_fp8_f32 v7, v8, v4 op_sel:[0,0,1]
	v_mul_f32_e32 v4, 0x43800000, v77
	v_mul_f32_e32 v8, 0x43800000, v81
	v_med3_f32 v4, v4, s0, v1
	v_med3_f32 v14, v8, s0, v1
	v_mov_b32_e32 v8, v5
	v_cvt_pk_fp8_f32 v8, v4, v14
	v_mul_f32_e32 v9, 0x43800000, v109
	v_mul_f32_e32 v4, 0x43800000, v89
	v_med3_f32 v9, v9, s0, v1
	v_med3_f32 v4, v4, s0, v1
	v_cvt_pk_fp8_f32 v8, v9, v4 op_sel:[0,0,1]
	v_mul_f32_e32 v4, 0x43800000, v137
	v_mul_f32_e32 v9, 0x43800000, v141
	v_med3_f32 v4, v4, s0, v1
	v_med3_f32 v15, v9, s0, v1
	v_mov_b32_e32 v9, v5
	v_cvt_pk_fp8_f32 v9, v4, v15
	v_mul_f32_e32 v14, 0x43800000, v149
	v_mul_f32_e32 v4, 0x43800000, v145
	v_med3_f32 v14, v14, s0, v1
	v_med3_f32 v4, v4, s0, v1
	v_cvt_pk_fp8_f32 v9, v14, v4 op_sel:[0,0,1]
	ds_write_b128 v166, v[102:105] offset:34816
	ds_write_b128 v166, v[114:117] offset:35088
	ds_write_b128 v166, v[122:125] offset:35360
	ds_write_b128 v166, v[6:9] offset:35632
	s_waitcnt lgkmcnt(0)
	s_barrier
	s_mov_b32 s1, 0x1400000
	v_add_co_u32_e32 v6, vcc, s1, v2
	s_mov_b32 s1, 0x1404000
	s_nop 0
	v_addc_co_u32_e32 v7, vcc, 0, v3, vcc
	v_add_co_u32_e32 v14, vcc, s1, v2
	s_mov_b32 s1, 0x1408000
	s_nop 0
	v_addc_co_u32_e32 v15, vcc, 0, v3, vcc
	v_add_co_u32_e32 v42, vcc, s1, v2
	s_mov_b32 s1, 0x140c000
	s_nop 0
	v_addc_co_u32_e32 v43, vcc, 0, v3, vcc
	v_add_co_u32_e32 v44, vcc, s1, v2
	s_mov_b32 s1, 0x1410000
	s_nop 0
	v_addc_co_u32_e32 v45, vcc, 0, v3, vcc
	v_add_co_u32_e32 v54, vcc, s1, v2
	s_mov_b32 s1, 0x1414000
	s_nop 0
	v_addc_co_u32_e32 v55, vcc, 0, v3, vcc
	v_add_co_u32_e32 v56, vcc, s1, v2
	s_mov_b32 s1, 0x1418000
	s_nop 0
	v_addc_co_u32_e32 v57, vcc, 0, v3, vcc
	v_add_co_u32_e32 v74, vcc, s1, v2
	s_mov_b32 s1, 0x141c000
	s_nop 0
	v_addc_co_u32_e32 v75, vcc, 0, v3, vcc
	v_add_co_u32_e32 v76, vcc, s1, v2
	s_mov_b32 s1, 0x1420000
	s_nop 0
	v_addc_co_u32_e32 v77, vcc, 0, v3, vcc
	v_add_co_u32_e32 v86, vcc, s1, v2
	s_mov_b32 s1, 0x1424000
	s_nop 0
	v_addc_co_u32_e32 v87, vcc, 0, v3, vcc
	v_add_co_u32_e32 v88, vcc, s1, v2
	s_mov_b32 s1, 0x1428000
	s_nop 0
	v_addc_co_u32_e32 v89, vcc, 0, v3, vcc
	global_load_dwordx4 v[6:9], v[6:7], off sc0 nt
	s_nop 0
	global_load_dwordx4 v[14:17], v[14:15], off sc0 nt
	s_nop 0
	global_load_dwordx4 v[30:33], v[42:43], off sc0 nt
	global_load_dwordx4 v[22:25], v[44:45], off sc0 nt
	s_nop 0
	global_load_dwordx4 v[42:45], v[54:55], off sc0 nt
	global_load_dwordx4 v[46:49], v[56:57], off sc0 nt
	global_load_dwordx4 v[62:65], v[74:75], off sc0 nt
	s_nop 0
	global_load_dwordx4 v[54:57], v[76:77], off sc0 nt
	s_nop 0
	global_load_dwordx4 v[74:77], v[86:87], off sc0 nt
	global_load_dwordx4 v[78:81], v[88:89], off sc0 nt
	v_add_co_u32_e32 v86, vcc, s1, v2
	s_mov_b32 s1, 0x142c000
	s_nop 0
	v_addc_co_u32_e32 v87, vcc, 0, v3, vcc
	v_add_co_u32_e32 v88, vcc, s1, v2
	s_mov_b32 s1, 0x1430000
	s_nop 0
	v_addc_co_u32_e32 v89, vcc, 0, v3, vcc
	v_add_co_u32_e32 v106, vcc, s1, v2
	s_mov_b32 s1, 0x1434000
	s_nop 0
	v_addc_co_u32_e32 v107, vcc, 0, v3, vcc
	v_add_co_u32_e32 v114, vcc, s1, v2
	s_mov_b32 s1, 0x1438000
	s_nop 0
	v_addc_co_u32_e32 v115, vcc, 0, v3, vcc
	v_add_co_u32_e32 v122, vcc, s1, v2
	s_mov_b32 s1, 0x143c000
	s_nop 0
	v_addc_co_u32_e32 v123, vcc, 0, v3, vcc
	v_add_co_u32_e32 v124, vcc, s1, v2
	global_load_dwordx4 v[102:105], v[86:87], off sc0 nt
	s_nop 0
	global_load_dwordx4 v[86:89], v[88:89], off sc0 nt
	v_addc_co_u32_e32 v125, vcc, 0, v3, vcc
	global_load_dwordx4 v[106:109], v[106:107], off sc0 nt
	s_nop 0
	global_load_dwordx4 v[114:117], v[114:115], off sc0 nt
	s_nop 0
	global_load_dwordx4 v[130:133], v[122:123], off sc0 nt
	s_nop 0
	global_load_dwordx4 v[122:125], v[124:125], off sc0 nt
	ds_read_b128 v[134:137], v154 offset:34816
	ds_read_b128 v[138:141], v156 offset:34816
	ds_read_b128 v[142:145], v158 offset:34816
	ds_read_b128 v[146:149], v162 offset:34816
	s_waitcnt lgkmcnt(3)
	global_store_dwordx4 v[150:151], v[134:137], off offset:768 nt
	s_waitcnt lgkmcnt(2)
	global_store_dwordx4 v[152:153], v[138:141], off offset:768 nt
	s_waitcnt lgkmcnt(1)
	global_store_dwordx4 v[160:161], v[142:145], off offset:768 nt
	s_waitcnt lgkmcnt(0)
	global_store_dwordx4 v[164:165], v[146:149], off offset:768 nt
	s_waitcnt vmcnt(39)
	v_mul_f32_e32 v4, 0x43800000, v10
	s_waitcnt vmcnt(38)
	v_mul_f32_e32 v10, 0x43800000, v18
	v_med3_f32 v4, v4, s0, v1
	v_med3_f32 v10, v10, s0, v1
	v_mov_b32_e32 v134, v5
	v_cvt_pk_fp8_f32 v134, v4, v10
	s_waitcnt vmcnt(37)
	v_mul_f32_e32 v18, 0x43800000, v34
	s_waitcnt vmcnt(36)
	v_mul_f32_e32 v4, 0x43800000, v26
	v_med3_f32 v10, v18, s0, v1
	v_med3_f32 v4, v4, s0, v1
	v_cvt_pk_fp8_f32 v134, v10, v4 op_sel:[0,0,1]
	s_waitcnt vmcnt(35)
	v_mul_f32_e32 v4, 0x43800000, v38
	s_waitcnt vmcnt(34)
	v_mul_f32_e32 v10, 0x43800000, v50
	v_med3_f32 v4, v4, s0, v1
	v_med3_f32 v10, v10, s0, v1
	v_mov_b32_e32 v135, v5
	v_cvt_pk_fp8_f32 v135, v4, v10
	s_waitcnt vmcnt(33)
	v_mul_f32_e32 v18, 0x43800000, v66
	s_waitcnt vmcnt(32)
	v_mul_f32_e32 v4, 0x43800000, v58
	v_med3_f32 v10, v18, s0, v1
	v_med3_f32 v4, v4, s0, v1
	v_cvt_pk_fp8_f32 v135, v10, v4 op_sel:[0,0,1]
	s_waitcnt vmcnt(31)
	v_mul_f32_e32 v4, 0x43800000, v70
	s_waitcnt vmcnt(30)
	v_mul_f32_e32 v10, 0x43800000, v82
	v_med3_f32 v4, v4, s0, v1
	v_med3_f32 v10, v10, s0, v1
	v_mov_b32_e32 v136, v5
	v_cvt_pk_fp8_f32 v136, v4, v10
	s_waitcnt vmcnt(29)
	v_mul_f32_e32 v18, 0x43800000, v94
	s_waitcnt vmcnt(28)
	v_mul_f32_e32 v4, 0x43800000, v90
	v_med3_f32 v10, v18, s0, v1
	v_med3_f32 v4, v4, s0, v1
	v_cvt_pk_fp8_f32 v136, v10, v4 op_sel:[0,0,1]
	s_waitcnt vmcnt(27)
	v_mul_f32_e32 v4, 0x43800000, v98
	s_waitcnt vmcnt(26)
	v_mul_f32_e32 v10, 0x43800000, v110
	v_med3_f32 v4, v4, s0, v1
	v_med3_f32 v10, v10, s0, v1
	v_mov_b32_e32 v137, v5
	v_cvt_pk_fp8_f32 v137, v4, v10
	s_waitcnt vmcnt(25)
	v_mul_f32_e32 v18, 0x43800000, v126
	s_waitcnt vmcnt(24)
	v_mul_f32_e32 v4, 0x43800000, v118
	v_med3_f32 v10, v18, s0, v1
	v_med3_f32 v4, v4, s0, v1
	v_cvt_pk_fp8_f32 v137, v10, v4 op_sel:[0,0,1]
	v_mul_f32_e32 v4, 0x43800000, v11
	v_mul_f32_e32 v10, 0x43800000, v19
	v_med3_f32 v4, v4, s0, v1
	v_med3_f32 v10, v10, s0, v1
	v_mov_b32_e32 v138, v5
	v_cvt_pk_fp8_f32 v138, v4, v10
	v_mul_f32_e32 v11, 0x43800000, v35
	v_mul_f32_e32 v4, 0x43800000, v27
	v_med3_f32 v10, v11, s0, v1
	v_med3_f32 v4, v4, s0, v1
	v_cvt_pk_fp8_f32 v138, v10, v4 op_sel:[0,0,1]
	v_mul_f32_e32 v4, 0x43800000, v39
	v_mul_f32_e32 v10, 0x43800000, v51
	v_med3_f32 v4, v4, s0, v1
	v_med3_f32 v10, v10, s0, v1
	v_mov_b32_e32 v139, v5
	v_cvt_pk_fp8_f32 v139, v4, v10
	v_mul_f32_e32 v11, 0x43800000, v67
	v_mul_f32_e32 v4, 0x43800000, v59
	v_med3_f32 v10, v11, s0, v1
	v_med3_f32 v4, v4, s0, v1
	v_cvt_pk_fp8_f32 v139, v10, v4 op_sel:[0,0,1]
	v_mul_f32_e32 v4, 0x43800000, v71
	v_mul_f32_e32 v10, 0x43800000, v83
	v_med3_f32 v4, v4, s0, v1
	v_med3_f32 v10, v10, s0, v1
	v_mov_b32_e32 v140, v5
	v_cvt_pk_fp8_f32 v140, v4, v10
	v_mul_f32_e32 v11, 0x43800000, v95
	v_mul_f32_e32 v4, 0x43800000, v91
	v_med3_f32 v10, v11, s0, v1
	v_med3_f32 v4, v4, s0, v1
	v_cvt_pk_fp8_f32 v140, v10, v4 op_sel:[0,0,1]
	v_mul_f32_e32 v4, 0x43800000, v99
	v_mul_f32_e32 v10, 0x43800000, v111
	v_med3_f32 v4, v4, s0, v1
	v_med3_f32 v10, v10, s0, v1
	v_mov_b32_e32 v141, v5
	v_cvt_pk_fp8_f32 v141, v4, v10
	v_mul_f32_e32 v11, 0x43800000, v127
	v_mul_f32_e32 v4, 0x43800000, v119
	v_med3_f32 v10, v11, s0, v1
	v_med3_f32 v4, v4, s0, v1
	v_cvt_pk_fp8_f32 v141, v10, v4 op_sel:[0,0,1]
	v_mul_f32_e32 v4, 0x43800000, v12
	v_mul_f32_e32 v10, 0x43800000, v20
	v_med3_f32 v4, v4, s0, v1
	v_med3_f32 v10, v10, s0, v1
	v_mov_b32_e32 v142, v5
	v_cvt_pk_fp8_f32 v142, v4, v10
	v_mul_f32_e32 v11, 0x43800000, v36
	v_mul_f32_e32 v4, 0x43800000, v28
	v_med3_f32 v10, v11, s0, v1
	v_med3_f32 v4, v4, s0, v1
	v_cvt_pk_fp8_f32 v142, v10, v4 op_sel:[0,0,1]
	v_mul_f32_e32 v4, 0x43800000, v40
	v_mul_f32_e32 v10, 0x43800000, v52
	v_med3_f32 v4, v4, s0, v1
	v_med3_f32 v10, v10, s0, v1
	v_mov_b32_e32 v143, v5
	v_cvt_pk_fp8_f32 v143, v4, v10
	v_mul_f32_e32 v11, 0x43800000, v68
	v_mul_f32_e32 v4, 0x43800000, v60
	v_med3_f32 v10, v11, s0, v1
	v_med3_f32 v4, v4, s0, v1
	v_cvt_pk_fp8_f32 v143, v10, v4 op_sel:[0,0,1]
	v_mul_f32_e32 v4, 0x43800000, v72
	v_mul_f32_e32 v10, 0x43800000, v84
	v_med3_f32 v4, v4, s0, v1
	v_med3_f32 v10, v10, s0, v1
	v_mov_b32_e32 v144, v5
	v_cvt_pk_fp8_f32 v144, v4, v10
	v_mul_f32_e32 v11, 0x43800000, v96
	v_mul_f32_e32 v4, 0x43800000, v92
	v_med3_f32 v10, v11, s0, v1
	v_med3_f32 v4, v4, s0, v1
	v_cvt_pk_fp8_f32 v144, v10, v4 op_sel:[0,0,1]
	v_mul_f32_e32 v4, 0x43800000, v100
	v_mul_f32_e32 v10, 0x43800000, v112
	v_med3_f32 v4, v4, s0, v1
	v_med3_f32 v10, v10, s0, v1
	v_mov_b32_e32 v145, v5
	v_cvt_pk_fp8_f32 v145, v4, v10
	v_mul_f32_e32 v11, 0x43800000, v128
	v_mul_f32_e32 v4, 0x43800000, v120
	v_med3_f32 v10, v11, s0, v1
	v_med3_f32 v4, v4, s0, v1
	v_cvt_pk_fp8_f32 v145, v10, v4 op_sel:[0,0,1]
	v_mul_f32_e32 v4, 0x43800000, v13
	v_mul_f32_e32 v10, 0x43800000, v21
	v_med3_f32 v4, v4, s0, v1
	v_med3_f32 v12, v10, s0, v1
	v_mov_b32_e32 v10, v5
	v_cvt_pk_fp8_f32 v10, v4, v12
	v_mul_f32_e32 v11, 0x43800000, v37
	v_mul_f32_e32 v4, 0x43800000, v29
	v_med3_f32 v11, v11, s0, v1
	v_med3_f32 v4, v4, s0, v1
	v_cvt_pk_fp8_f32 v10, v11, v4 op_sel:[0,0,1]
	v_mul_f32_e32 v4, 0x43800000, v41
	v_mul_f32_e32 v11, 0x43800000, v53
	v_med3_f32 v4, v4, s0, v1
	v_med3_f32 v13, v11, s0, v1
	v_mov_b32_e32 v11, v5
	v_cvt_pk_fp8_f32 v11, v4, v13
	v_mul_f32_e32 v12, 0x43800000, v69
	v_mul_f32_e32 v4, 0x43800000, v61
	v_med3_f32 v12, v12, s0, v1
	v_med3_f32 v4, v4, s0, v1
	v_cvt_pk_fp8_f32 v11, v12, v4 op_sel:[0,0,1]
	v_mul_f32_e32 v4, 0x43800000, v73
	v_mul_f32_e32 v12, 0x43800000, v85
	v_med3_f32 v4, v4, s0, v1
	v_med3_f32 v18, v12, s0, v1
	v_mov_b32_e32 v12, v5
	v_cvt_pk_fp8_f32 v12, v4, v18
	v_mul_f32_e32 v13, 0x43800000, v97
	v_mul_f32_e32 v4, 0x43800000, v93
	v_med3_f32 v13, v13, s0, v1
	v_med3_f32 v4, v4, s0, v1
	v_cvt_pk_fp8_f32 v12, v13, v4 op_sel:[0,0,1]
	v_mul_f32_e32 v4, 0x43800000, v101
	v_mul_f32_e32 v13, 0x43800000, v113
	v_med3_f32 v4, v4, s0, v1
	v_med3_f32 v19, v13, s0, v1
	v_mov_b32_e32 v13, v5
	v_cvt_pk_fp8_f32 v13, v4, v19
	v_mul_f32_e32 v18, 0x43800000, v129
	v_mul_f32_e32 v4, 0x43800000, v121
	v_med3_f32 v18, v18, s0, v1
	v_med3_f32 v4, v4, s0, v1
	v_cvt_pk_fp8_f32 v13, v18, v4 op_sel:[0,0,1]
	ds_write_b128 v166, v[134:137]
	ds_write_b128 v166, v[138:141] offset:272
	ds_write_b128 v166, v[142:145] offset:544
	ds_write_b128 v166, v[10:13] offset:816
	s_waitcnt lgkmcnt(0)
	s_barrier
	s_mov_b32 s1, 0x1800000
	v_add_co_u32_e32 v10, vcc, s1, v2
	s_mov_b32 s1, 0x1804000
	s_nop 0
	v_addc_co_u32_e32 v11, vcc, 0, v3, vcc
	v_add_co_u32_e32 v18, vcc, s1, v2
	s_mov_b32 s1, 0x1808000
	s_nop 0
	v_addc_co_u32_e32 v19, vcc, 0, v3, vcc
	v_add_co_u32_e32 v38, vcc, s1, v2
	s_mov_b32 s1, 0x180c000
	s_nop 0
	v_addc_co_u32_e32 v39, vcc, 0, v3, vcc
	v_add_co_u32_e32 v40, vcc, s1, v2
	s_mov_b32 s1, 0x1810000
	s_nop 0
	v_addc_co_u32_e32 v41, vcc, 0, v3, vcc
	v_add_co_u32_e32 v58, vcc, s1, v2
	s_mov_b32 s1, 0x1814000
	s_nop 0
	v_addc_co_u32_e32 v59, vcc, 0, v3, vcc
	v_add_co_u32_e32 v60, vcc, s1, v2
	s_mov_b32 s1, 0x1818000
	s_nop 0
	v_addc_co_u32_e32 v61, vcc, 0, v3, vcc
	v_add_co_u32_e32 v70, vcc, s1, v2
	s_mov_b32 s1, 0x181c000
	s_nop 0
	v_addc_co_u32_e32 v71, vcc, 0, v3, vcc
	v_add_co_u32_e32 v72, vcc, s1, v2
	s_mov_b32 s1, 0x1820000
	s_nop 0
	v_addc_co_u32_e32 v73, vcc, 0, v3, vcc
	v_add_co_u32_e32 v90, vcc, s1, v2
	s_mov_b32 s1, 0x1824000
	s_nop 0
	v_addc_co_u32_e32 v91, vcc, 0, v3, vcc
	v_add_co_u32_e32 v92, vcc, s1, v2
	s_mov_b32 s1, 0x1828000
	s_nop 0
	v_addc_co_u32_e32 v93, vcc, 0, v3, vcc
	global_load_dwordx4 v[10:13], v[10:11], off sc0 nt
	s_nop 0
	global_load_dwordx4 v[18:21], v[18:19], off sc0 nt
	s_nop 0
	global_load_dwordx4 v[34:37], v[38:39], off sc0 nt
	global_load_dwordx4 v[26:29], v[40:41], off sc0 nt
	s_nop 0
	global_load_dwordx4 v[38:41], v[58:59], off sc0 nt
	global_load_dwordx4 v[50:53], v[60:61], off sc0 nt
	global_load_dwordx4 v[66:69], v[70:71], off sc0 nt
	s_nop 0
	global_load_dwordx4 v[58:61], v[72:73], off sc0 nt
	s_nop 0
	global_load_dwordx4 v[70:73], v[90:91], off sc0 nt
	global_load_dwordx4 v[82:85], v[92:93], off sc0 nt
	v_add_co_u32_e32 v90, vcc, s1, v2
	s_mov_b32 s1, 0x182c000
	s_nop 0
	v_addc_co_u32_e32 v91, vcc, 0, v3, vcc
	v_add_co_u32_e32 v92, vcc, s1, v2
	s_mov_b32 s1, 0x1830000
	s_nop 0
	v_addc_co_u32_e32 v93, vcc, 0, v3, vcc
	v_add_co_u32_e32 v98, vcc, s1, v2
	s_mov_b32 s1, 0x1834000
	s_nop 0
	v_addc_co_u32_e32 v99, vcc, 0, v3, vcc
	v_add_co_u32_e32 v110, vcc, s1, v2
	s_mov_b32 s1, 0x1838000
	s_nop 0
	v_addc_co_u32_e32 v111, vcc, 0, v3, vcc
	v_add_co_u32_e32 v118, vcc, s1, v2
	s_mov_b32 s1, 0x183c000
	s_nop 0
	v_addc_co_u32_e32 v119, vcc, 0, v3, vcc
	v_add_co_u32_e32 v120, vcc, s1, v2
	global_load_dwordx4 v[94:97], v[90:91], off sc0 nt
	s_nop 0
	global_load_dwordx4 v[90:93], v[92:93], off sc0 nt
	v_addc_co_u32_e32 v121, vcc, 0, v3, vcc
	global_load_dwordx4 v[98:101], v[98:99], off sc0 nt
	s_nop 0
	global_load_dwordx4 v[110:113], v[110:111], off sc0 nt
	s_nop 0
	global_load_dwordx4 v[126:129], v[118:119], off sc0 nt
	s_nop 0
	global_load_dwordx4 v[118:121], v[120:121], off sc0 nt
	ds_read_b128 v[134:137], v154
	ds_read_b128 v[138:141], v156
	ds_read_b128 v[142:145], v158
	ds_read_b128 v[146:149], v162
	s_waitcnt lgkmcnt(3)
	global_store_dwordx4 v[150:151], v[134:137], off offset:1024 nt
	s_waitcnt lgkmcnt(2)
	global_store_dwordx4 v[152:153], v[138:141], off offset:1024 nt
	s_waitcnt lgkmcnt(1)
	global_store_dwordx4 v[160:161], v[142:145], off offset:1024 nt
	s_waitcnt lgkmcnt(0)
	global_store_dwordx4 v[164:165], v[146:149], off offset:1024 nt
	s_waitcnt vmcnt(39)
	v_mul_f32_e32 v4, 0x43800000, v6
	s_waitcnt vmcnt(38)
	v_mul_f32_e32 v6, 0x43800000, v14
	v_med3_f32 v4, v4, s0, v1
	v_med3_f32 v6, v6, s0, v1
	v_mov_b32_e32 v134, v5
	v_cvt_pk_fp8_f32 v134, v4, v6
	s_waitcnt vmcnt(37)
	v_mul_f32_e32 v14, 0x43800000, v30
	s_waitcnt vmcnt(36)
	v_mul_f32_e32 v4, 0x43800000, v22
	v_med3_f32 v6, v14, s0, v1
	v_med3_f32 v4, v4, s0, v1
	v_cvt_pk_fp8_f32 v134, v6, v4 op_sel:[0,0,1]
	s_waitcnt vmcnt(35)
	v_mul_f32_e32 v4, 0x43800000, v42
	s_waitcnt vmcnt(34)
	v_mul_f32_e32 v6, 0x43800000, v46
	v_med3_f32 v4, v4, s0, v1
	v_med3_f32 v6, v6, s0, v1
	v_mov_b32_e32 v135, v5
	v_cvt_pk_fp8_f32 v135, v4, v6
	s_waitcnt vmcnt(33)
	v_mul_f32_e32 v14, 0x43800000, v62
	s_waitcnt vmcnt(32)
	v_mul_f32_e32 v4, 0x43800000, v54
	v_med3_f32 v6, v14, s0, v1
	v_med3_f32 v4, v4, s0, v1
	v_cvt_pk_fp8_f32 v135, v6, v4 op_sel:[0,0,1]
	s_waitcnt vmcnt(31)
	v_mul_f32_e32 v4, 0x43800000, v74
	s_waitcnt vmcnt(30)
	v_mul_f32_e32 v6, 0x43800000, v78
	v_med3_f32 v4, v4, s0, v1
	v_med3_f32 v6, v6, s0, v1
	v_mov_b32_e32 v136, v5
	v_cvt_pk_fp8_f32 v136, v4, v6
	s_waitcnt vmcnt(29)
	v_mul_f32_e32 v14, 0x43800000, v102
	s_waitcnt vmcnt(28)
	v_mul_f32_e32 v4, 0x43800000, v86
	v_med3_f32 v6, v14, s0, v1
	v_med3_f32 v4, v4, s0, v1
	v_cvt_pk_fp8_f32 v136, v6, v4 op_sel:[0,0,1]
	s_waitcnt vmcnt(27)
	v_mul_f32_e32 v4, 0x43800000, v106
	s_waitcnt vmcnt(26)
	v_mul_f32_e32 v6, 0x43800000, v114
	v_med3_f32 v4, v4, s0, v1
	v_med3_f32 v6, v6, s0, v1
	v_mov_b32_e32 v137, v5
	v_cvt_pk_fp8_f32 v137, v4, v6
	s_waitcnt vmcnt(25)
	v_mul_f32_e32 v14, 0x43800000, v130
	s_waitcnt vmcnt(24)
	v_mul_f32_e32 v4, 0x43800000, v122
	v_med3_f32 v6, v14, s0, v1
	v_med3_f32 v4, v4, s0, v1
	v_cvt_pk_fp8_f32 v137, v6, v4 op_sel:[0,0,1]
	v_mul_f32_e32 v4, 0x43800000, v7
	v_mul_f32_e32 v6, 0x43800000, v15
	v_med3_f32 v4, v4, s0, v1
	v_med3_f32 v6, v6, s0, v1
	v_mov_b32_e32 v138, v5
	v_cvt_pk_fp8_f32 v138, v4, v6
	v_mul_f32_e32 v7, 0x43800000, v31
	v_mul_f32_e32 v4, 0x43800000, v23
	v_med3_f32 v6, v7, s0, v1
	v_med3_f32 v4, v4, s0, v1
	v_cvt_pk_fp8_f32 v138, v6, v4 op_sel:[0,0,1]
	v_mul_f32_e32 v4, 0x43800000, v43
	v_mul_f32_e32 v6, 0x43800000, v47
	v_med3_f32 v4, v4, s0, v1
	v_med3_f32 v6, v6, s0, v1
	v_mov_b32_e32 v139, v5
	v_cvt_pk_fp8_f32 v139, v4, v6
	v_mul_f32_e32 v7, 0x43800000, v63
	v_mul_f32_e32 v4, 0x43800000, v55
	v_med3_f32 v6, v7, s0, v1
	v_med3_f32 v4, v4, s0, v1
	v_cvt_pk_fp8_f32 v139, v6, v4 op_sel:[0,0,1]
	v_mul_f32_e32 v4, 0x43800000, v75
	v_mul_f32_e32 v6, 0x43800000, v79
	v_med3_f32 v4, v4, s0, v1
	v_med3_f32 v6, v6, s0, v1
	v_mov_b32_e32 v140, v5
	v_cvt_pk_fp8_f32 v140, v4, v6
	v_mul_f32_e32 v7, 0x43800000, v103
	v_mul_f32_e32 v4, 0x43800000, v87
	v_med3_f32 v6, v7, s0, v1
	v_med3_f32 v4, v4, s0, v1
	v_cvt_pk_fp8_f32 v140, v6, v4 op_sel:[0,0,1]
	v_mul_f32_e32 v4, 0x43800000, v107
	v_mul_f32_e32 v6, 0x43800000, v115
	v_med3_f32 v4, v4, s0, v1
	v_med3_f32 v6, v6, s0, v1
	v_mov_b32_e32 v141, v5
	v_cvt_pk_fp8_f32 v141, v4, v6
	v_mul_f32_e32 v7, 0x43800000, v131
	v_mul_f32_e32 v4, 0x43800000, v123
	v_med3_f32 v6, v7, s0, v1
	v_med3_f32 v4, v4, s0, v1
	v_cvt_pk_fp8_f32 v141, v6, v4 op_sel:[0,0,1]
	v_mul_f32_e32 v4, 0x43800000, v8
	v_mul_f32_e32 v6, 0x43800000, v16
	v_med3_f32 v4, v4, s0, v1
	v_med3_f32 v6, v6, s0, v1
	v_mov_b32_e32 v142, v5
	v_cvt_pk_fp8_f32 v142, v4, v6
	v_mul_f32_e32 v7, 0x43800000, v32
	v_mul_f32_e32 v4, 0x43800000, v24
	v_med3_f32 v6, v7, s0, v1
	v_med3_f32 v4, v4, s0, v1
	v_cvt_pk_fp8_f32 v142, v6, v4 op_sel:[0,0,1]
	v_mul_f32_e32 v4, 0x43800000, v44
	v_mul_f32_e32 v6, 0x43800000, v48
	v_med3_f32 v4, v4, s0, v1
	v_med3_f32 v6, v6, s0, v1
	v_mov_b32_e32 v143, v5
	v_cvt_pk_fp8_f32 v143, v4, v6
	v_mul_f32_e32 v7, 0x43800000, v64
	v_mul_f32_e32 v4, 0x43800000, v56
	v_med3_f32 v6, v7, s0, v1
	v_med3_f32 v4, v4, s0, v1
	v_cvt_pk_fp8_f32 v143, v6, v4 op_sel:[0,0,1]
	v_mul_f32_e32 v4, 0x43800000, v76
	v_mul_f32_e32 v6, 0x43800000, v80
	v_med3_f32 v4, v4, s0, v1
	v_med3_f32 v6, v6, s0, v1
	v_mov_b32_e32 v144, v5
	v_cvt_pk_fp8_f32 v144, v4, v6
	v_mul_f32_e32 v7, 0x43800000, v104
	v_mul_f32_e32 v4, 0x43800000, v88
	v_med3_f32 v6, v7, s0, v1
	v_med3_f32 v4, v4, s0, v1
	v_cvt_pk_fp8_f32 v144, v6, v4 op_sel:[0,0,1]
	v_mul_f32_e32 v4, 0x43800000, v108
	v_mul_f32_e32 v6, 0x43800000, v116
	v_med3_f32 v4, v4, s0, v1
	v_med3_f32 v6, v6, s0, v1
	v_mov_b32_e32 v145, v5
	v_cvt_pk_fp8_f32 v145, v4, v6
	v_mul_f32_e32 v7, 0x43800000, v132
	v_mul_f32_e32 v4, 0x43800000, v124
	v_med3_f32 v6, v7, s0, v1
	v_med3_f32 v4, v4, s0, v1
	v_cvt_pk_fp8_f32 v145, v6, v4 op_sel:[0,0,1]
	v_mul_f32_e32 v4, 0x43800000, v9
	v_mul_f32_e32 v6, 0x43800000, v17
	v_med3_f32 v4, v4, s0, v1
	v_med3_f32 v8, v6, s0, v1
	v_mov_b32_e32 v6, v5
	v_cvt_pk_fp8_f32 v6, v4, v8
	v_mul_f32_e32 v7, 0x43800000, v33
	v_mul_f32_e32 v4, 0x43800000, v25
	v_med3_f32 v7, v7, s0, v1
	v_med3_f32 v4, v4, s0, v1
	v_cvt_pk_fp8_f32 v6, v7, v4 op_sel:[0,0,1]
	v_mul_f32_e32 v4, 0x43800000, v45
	v_mul_f32_e32 v7, 0x43800000, v49
	v_med3_f32 v4, v4, s0, v1
	v_med3_f32 v9, v7, s0, v1
	v_mov_b32_e32 v7, v5
	v_cvt_pk_fp8_f32 v7, v4, v9
	v_mul_f32_e32 v8, 0x43800000, v65
	v_mul_f32_e32 v4, 0x43800000, v57
	v_med3_f32 v8, v8, s0, v1
	v_med3_f32 v4, v4, s0, v1
	v_cvt_pk_fp8_f32 v7, v8, v4 op_sel:[0,0,1]
	v_mul_f32_e32 v4, 0x43800000, v77
	v_mul_f32_e32 v8, 0x43800000, v81
	v_med3_f32 v4, v4, s0, v1
	v_med3_f32 v14, v8, s0, v1
	v_mov_b32_e32 v8, v5
	v_cvt_pk_fp8_f32 v8, v4, v14
	v_mul_f32_e32 v9, 0x43800000, v105
	v_mul_f32_e32 v4, 0x43800000, v89
	v_med3_f32 v9, v9, s0, v1
	v_med3_f32 v4, v4, s0, v1
	v_cvt_pk_fp8_f32 v8, v9, v4 op_sel:[0,0,1]
	v_mul_f32_e32 v4, 0x43800000, v109
	v_mul_f32_e32 v9, 0x43800000, v117
	v_med3_f32 v4, v4, s0, v1
	v_med3_f32 v15, v9, s0, v1
	v_mov_b32_e32 v9, v5
	v_cvt_pk_fp8_f32 v9, v4, v15
	v_mul_f32_e32 v14, 0x43800000, v133
	v_mul_f32_e32 v4, 0x43800000, v125
	v_med3_f32 v14, v14, s0, v1
	v_med3_f32 v4, v4, s0, v1
	v_cvt_pk_fp8_f32 v9, v14, v4 op_sel:[0,0,1]
	ds_write_b128 v166, v[134:137] offset:34816
	ds_write_b128 v166, v[138:141] offset:35088
	ds_write_b128 v166, v[142:145] offset:35360
	ds_write_b128 v166, v[6:9] offset:35632
	s_waitcnt lgkmcnt(0)
	s_barrier
	s_mov_b32 s1, 0x1c00000
	v_add_co_u32_e32 v6, vcc, s1, v2
	s_mov_b32 s1, 0x1c04000
	s_nop 0
	v_addc_co_u32_e32 v7, vcc, 0, v3, vcc
	v_add_co_u32_e32 v14, vcc, s1, v2
	s_mov_b32 s1, 0x1c08000
	s_nop 0
	v_addc_co_u32_e32 v15, vcc, 0, v3, vcc
	v_add_co_u32_e32 v42, vcc, s1, v2
	s_mov_b32 s1, 0x1c0c000
	s_nop 0
	v_addc_co_u32_e32 v43, vcc, 0, v3, vcc
	v_add_co_u32_e32 v44, vcc, s1, v2
	s_mov_b32 s1, 0x1c10000
	s_nop 0
	v_addc_co_u32_e32 v45, vcc, 0, v3, vcc
	v_add_co_u32_e32 v54, vcc, s1, v2
	s_mov_b32 s1, 0x1c14000
	s_nop 0
	v_addc_co_u32_e32 v55, vcc, 0, v3, vcc
	v_add_co_u32_e32 v56, vcc, s1, v2
	s_mov_b32 s1, 0x1c18000
	s_nop 0
	v_addc_co_u32_e32 v57, vcc, 0, v3, vcc
	v_add_co_u32_e32 v74, vcc, s1, v2
	s_mov_b32 s1, 0x1c1c000
	s_nop 0
	v_addc_co_u32_e32 v75, vcc, 0, v3, vcc
	v_add_co_u32_e32 v76, vcc, s1, v2
	s_mov_b32 s1, 0x1c20000
	s_nop 0
	v_addc_co_u32_e32 v77, vcc, 0, v3, vcc
	v_add_co_u32_e32 v86, vcc, s1, v2
	s_mov_b32 s1, 0x1c24000
	s_nop 0
	v_addc_co_u32_e32 v87, vcc, 0, v3, vcc
	v_add_co_u32_e32 v88, vcc, s1, v2
	s_mov_b32 s1, 0x1c28000
	s_nop 0
	v_addc_co_u32_e32 v89, vcc, 0, v3, vcc
	global_load_dwordx4 v[6:9], v[6:7], off sc0 nt
	s_nop 0
	global_load_dwordx4 v[14:17], v[14:15], off sc0 nt
	s_nop 0
	global_load_dwordx4 v[30:33], v[42:43], off sc0 nt
	global_load_dwordx4 v[22:25], v[44:45], off sc0 nt
	s_nop 0
	global_load_dwordx4 v[42:45], v[54:55], off sc0 nt
	global_load_dwordx4 v[46:49], v[56:57], off sc0 nt
	global_load_dwordx4 v[62:65], v[74:75], off sc0 nt
	s_nop 0
	global_load_dwordx4 v[54:57], v[76:77], off sc0 nt
	s_nop 0
	global_load_dwordx4 v[74:77], v[86:87], off sc0 nt
	global_load_dwordx4 v[78:81], v[88:89], off sc0 nt
	v_add_co_u32_e32 v86, vcc, s1, v2
	s_mov_b32 s1, 0x1c2c000
	s_nop 0
	v_addc_co_u32_e32 v87, vcc, 0, v3, vcc
	v_add_co_u32_e32 v88, vcc, s1, v2
	s_mov_b32 s1, 0x1c30000
	s_nop 0
	v_addc_co_u32_e32 v89, vcc, 0, v3, vcc
	v_add_co_u32_e32 v106, vcc, s1, v2
	s_mov_b32 s1, 0x1c34000
	s_nop 0
	v_addc_co_u32_e32 v107, vcc, 0, v3, vcc
	v_add_co_u32_e32 v114, vcc, s1, v2
	s_mov_b32 s1, 0x1c38000
	s_nop 0
	v_addc_co_u32_e32 v115, vcc, 0, v3, vcc
	v_add_co_u32_e32 v122, vcc, s1, v2
	s_mov_b32 s1, 0x1c3c000
	s_nop 0
	v_addc_co_u32_e32 v123, vcc, 0, v3, vcc
	v_add_co_u32_e32 v2, vcc, s1, v2
	global_load_dwordx4 v[102:105], v[86:87], off sc0 nt
	s_nop 0
	global_load_dwordx4 v[86:89], v[88:89], off sc0 nt
	s_nop 0
	global_load_dwordx4 v[106:109], v[106:107], off sc0 nt
	s_nop 0
	global_load_dwordx4 v[114:117], v[114:115], off sc0 nt
	v_addc_co_u32_e32 v3, vcc, 0, v3, vcc
	global_load_dwordx4 v[130:133], v[122:123], off sc0 nt
	s_nop 0
	global_load_dwordx4 v[122:125], v[2:3], off sc0 nt
	ds_read_b128 v[134:137], v154 offset:34816
	ds_read_b128 v[138:141], v156 offset:34816
	ds_read_b128 v[142:145], v158 offset:34816
	ds_read_b128 v[146:149], v162 offset:34816
	s_waitcnt lgkmcnt(3)
	global_store_dwordx4 v[150:151], v[134:137], off offset:1280 nt
	s_waitcnt lgkmcnt(2)
	global_store_dwordx4 v[152:153], v[138:141], off offset:1280 nt
	s_waitcnt lgkmcnt(1)
	global_store_dwordx4 v[160:161], v[142:145], off offset:1280 nt
	s_waitcnt lgkmcnt(0)
	global_store_dwordx4 v[164:165], v[146:149], off offset:1280 nt
	s_waitcnt vmcnt(39)
	v_mul_f32_e32 v2, 0x43800000, v10
	s_waitcnt vmcnt(38)
	v_mul_f32_e32 v3, 0x43800000, v18
	v_med3_f32 v2, v2, s0, v1
	v_med3_f32 v3, v3, s0, v1
	v_mov_b32_e32 v134, v5
	v_cvt_pk_fp8_f32 v134, v2, v3
	s_waitcnt vmcnt(37)
	v_mul_f32_e32 v4, 0x43800000, v34
	s_waitcnt vmcnt(36)
	v_mul_f32_e32 v2, 0x43800000, v26
	v_med3_f32 v3, v4, s0, v1
	v_med3_f32 v2, v2, s0, v1
	v_cvt_pk_fp8_f32 v134, v3, v2 op_sel:[0,0,1]
	s_waitcnt vmcnt(35)
	v_mul_f32_e32 v2, 0x43800000, v38
	s_waitcnt vmcnt(34)
	v_mul_f32_e32 v3, 0x43800000, v50
	v_med3_f32 v2, v2, s0, v1
	v_med3_f32 v3, v3, s0, v1
	v_mov_b32_e32 v135, v5
	v_cvt_pk_fp8_f32 v135, v2, v3
	s_waitcnt vmcnt(33)
	v_mul_f32_e32 v4, 0x43800000, v66
	s_waitcnt vmcnt(32)
	v_mul_f32_e32 v2, 0x43800000, v58
	v_med3_f32 v3, v4, s0, v1
	v_med3_f32 v2, v2, s0, v1
	v_cvt_pk_fp8_f32 v135, v3, v2 op_sel:[0,0,1]
	s_waitcnt vmcnt(31)
	v_mul_f32_e32 v2, 0x43800000, v70
	s_waitcnt vmcnt(30)
	v_mul_f32_e32 v3, 0x43800000, v82
	v_med3_f32 v2, v2, s0, v1
	v_med3_f32 v3, v3, s0, v1
	v_mov_b32_e32 v136, v5
	v_cvt_pk_fp8_f32 v136, v2, v3
	s_waitcnt vmcnt(29)
	v_mul_f32_e32 v4, 0x43800000, v94
	s_waitcnt vmcnt(28)
	v_mul_f32_e32 v2, 0x43800000, v90
	v_med3_f32 v3, v4, s0, v1
	v_med3_f32 v2, v2, s0, v1
	v_cvt_pk_fp8_f32 v136, v3, v2 op_sel:[0,0,1]
	s_waitcnt vmcnt(27)
	v_mul_f32_e32 v2, 0x43800000, v98
	s_waitcnt vmcnt(26)
	v_mul_f32_e32 v3, 0x43800000, v110
	v_med3_f32 v2, v2, s0, v1
	v_med3_f32 v3, v3, s0, v1
	v_mov_b32_e32 v137, v5
	v_cvt_pk_fp8_f32 v137, v2, v3
	s_waitcnt vmcnt(25)
	v_mul_f32_e32 v4, 0x43800000, v126
	s_waitcnt vmcnt(24)
	v_mul_f32_e32 v2, 0x43800000, v118
	v_med3_f32 v3, v4, s0, v1
	v_med3_f32 v2, v2, s0, v1
	v_cvt_pk_fp8_f32 v137, v3, v2 op_sel:[0,0,1]
	v_mul_f32_e32 v2, 0x43800000, v11
	v_mul_f32_e32 v3, 0x43800000, v19
	v_med3_f32 v2, v2, s0, v1
	v_med3_f32 v3, v3, s0, v1
	v_mov_b32_e32 v138, v5
	v_cvt_pk_fp8_f32 v138, v2, v3
	v_mul_f32_e32 v4, 0x43800000, v35
	v_mul_f32_e32 v2, 0x43800000, v27
	v_med3_f32 v3, v4, s0, v1
	v_med3_f32 v2, v2, s0, v1
	v_cvt_pk_fp8_f32 v138, v3, v2 op_sel:[0,0,1]
	v_mul_f32_e32 v2, 0x43800000, v39
	v_mul_f32_e32 v3, 0x43800000, v51
	v_med3_f32 v2, v2, s0, v1
	v_med3_f32 v3, v3, s0, v1
	v_mov_b32_e32 v139, v5
	v_cvt_pk_fp8_f32 v139, v2, v3
	v_mul_f32_e32 v4, 0x43800000, v67
	v_mul_f32_e32 v2, 0x43800000, v59
	v_med3_f32 v3, v4, s0, v1
	v_med3_f32 v2, v2, s0, v1
	v_cvt_pk_fp8_f32 v139, v3, v2 op_sel:[0,0,1]
	v_mul_f32_e32 v2, 0x43800000, v71
	v_mul_f32_e32 v3, 0x43800000, v83
	v_med3_f32 v2, v2, s0, v1
	v_med3_f32 v3, v3, s0, v1
	v_mov_b32_e32 v140, v5
	v_cvt_pk_fp8_f32 v140, v2, v3
	v_mul_f32_e32 v4, 0x43800000, v95
	v_mul_f32_e32 v2, 0x43800000, v91
	v_med3_f32 v3, v4, s0, v1
	v_med3_f32 v2, v2, s0, v1
	v_cvt_pk_fp8_f32 v140, v3, v2 op_sel:[0,0,1]
	v_mul_f32_e32 v2, 0x43800000, v99
	v_mul_f32_e32 v3, 0x43800000, v111
	v_med3_f32 v2, v2, s0, v1
	v_med3_f32 v3, v3, s0, v1
	v_mov_b32_e32 v141, v5
	v_cvt_pk_fp8_f32 v141, v2, v3
	v_mul_f32_e32 v4, 0x43800000, v127
	v_mul_f32_e32 v2, 0x43800000, v119
	v_med3_f32 v3, v4, s0, v1
	v_med3_f32 v2, v2, s0, v1
	v_cvt_pk_fp8_f32 v141, v3, v2 op_sel:[0,0,1]
	v_mul_f32_e32 v2, 0x43800000, v12
	v_mul_f32_e32 v3, 0x43800000, v20
	v_med3_f32 v2, v2, s0, v1
	v_med3_f32 v3, v3, s0, v1
	v_mov_b32_e32 v142, v5
	v_cvt_pk_fp8_f32 v142, v2, v3
	v_mul_f32_e32 v4, 0x43800000, v36
	v_mul_f32_e32 v2, 0x43800000, v28
	v_med3_f32 v3, v4, s0, v1
	v_med3_f32 v2, v2, s0, v1
	v_cvt_pk_fp8_f32 v142, v3, v2 op_sel:[0,0,1]
	v_mul_f32_e32 v2, 0x43800000, v40
	v_mul_f32_e32 v3, 0x43800000, v52
	v_med3_f32 v2, v2, s0, v1
	v_med3_f32 v3, v3, s0, v1
	v_mov_b32_e32 v143, v5
	v_cvt_pk_fp8_f32 v143, v2, v3
	v_mul_f32_e32 v4, 0x43800000, v68
	v_mul_f32_e32 v2, 0x43800000, v60
	v_med3_f32 v3, v4, s0, v1
	v_med3_f32 v2, v2, s0, v1
	v_cvt_pk_fp8_f32 v143, v3, v2 op_sel:[0,0,1]
	v_mul_f32_e32 v2, 0x43800000, v72
	v_mul_f32_e32 v3, 0x43800000, v84
	v_med3_f32 v2, v2, s0, v1
	v_med3_f32 v3, v3, s0, v1
	v_mov_b32_e32 v144, v5
	v_cvt_pk_fp8_f32 v144, v2, v3
	v_mul_f32_e32 v4, 0x43800000, v96
	v_mul_f32_e32 v2, 0x43800000, v92
	v_med3_f32 v3, v4, s0, v1
	v_med3_f32 v2, v2, s0, v1
	v_cvt_pk_fp8_f32 v144, v3, v2 op_sel:[0,0,1]
	v_mul_f32_e32 v2, 0x43800000, v100
	v_mul_f32_e32 v3, 0x43800000, v112
	v_med3_f32 v2, v2, s0, v1
	v_med3_f32 v3, v3, s0, v1
	v_mov_b32_e32 v145, v5
	v_cvt_pk_fp8_f32 v145, v2, v3
	v_mul_f32_e32 v4, 0x43800000, v128
	v_mul_f32_e32 v2, 0x43800000, v120
	v_med3_f32 v3, v4, s0, v1
	v_med3_f32 v2, v2, s0, v1
	v_cvt_pk_fp8_f32 v145, v3, v2 op_sel:[0,0,1]
	v_mul_f32_e32 v2, 0x43800000, v13
	v_mul_f32_e32 v3, 0x43800000, v21
	v_med3_f32 v2, v2, s0, v1
	v_med3_f32 v3, v3, s0, v1
	v_mov_b32_e32 v10, v5
	v_cvt_pk_fp8_f32 v10, v2, v3
	v_mul_f32_e32 v4, 0x43800000, v37
	v_mul_f32_e32 v2, 0x43800000, v29
	v_med3_f32 v3, v4, s0, v1
	v_med3_f32 v2, v2, s0, v1
	v_cvt_pk_fp8_f32 v10, v3, v2 op_sel:[0,0,1]
	v_mul_f32_e32 v2, 0x43800000, v41
	v_mul_f32_e32 v3, 0x43800000, v53
	v_med3_f32 v2, v2, s0, v1
	v_med3_f32 v3, v3, s0, v1
	v_mov_b32_e32 v11, v5
	v_cvt_pk_fp8_f32 v11, v2, v3
	v_mul_f32_e32 v4, 0x43800000, v69
	v_mul_f32_e32 v2, 0x43800000, v61
	v_med3_f32 v3, v4, s0, v1
	v_med3_f32 v2, v2, s0, v1
	v_cvt_pk_fp8_f32 v11, v3, v2 op_sel:[0,0,1]
	v_mul_f32_e32 v2, 0x43800000, v73
	v_mul_f32_e32 v3, 0x43800000, v85
	v_med3_f32 v2, v2, s0, v1
	v_med3_f32 v3, v3, s0, v1
	v_mov_b32_e32 v12, v5
	v_cvt_pk_fp8_f32 v12, v2, v3
	v_mul_f32_e32 v4, 0x43800000, v97
	v_mul_f32_e32 v2, 0x43800000, v93
	v_med3_f32 v3, v4, s0, v1
	v_med3_f32 v2, v2, s0, v1
	v_cvt_pk_fp8_f32 v12, v3, v2 op_sel:[0,0,1]
	v_mul_f32_e32 v2, 0x43800000, v101
	v_mul_f32_e32 v3, 0x43800000, v113
	v_med3_f32 v2, v2, s0, v1
	v_med3_f32 v3, v3, s0, v1
	v_mov_b32_e32 v13, v5
	v_cvt_pk_fp8_f32 v13, v2, v3
	v_mul_f32_e32 v4, 0x43800000, v129
	v_mul_f32_e32 v2, 0x43800000, v121
	v_med3_f32 v3, v4, s0, v1
	v_med3_f32 v2, v2, s0, v1
	v_cvt_pk_fp8_f32 v13, v3, v2 op_sel:[0,0,1]
	ds_write_b128 v166, v[134:137]
	ds_write_b128 v166, v[138:141] offset:272
	ds_write_b128 v166, v[142:145] offset:544
	ds_write_b128 v166, v[10:13] offset:816
	s_waitcnt lgkmcnt(0)
	s_barrier
	ds_read_b128 v[10:13], v154
	ds_read_b128 v[18:21], v156
	ds_read_b128 v[26:29], v158
	ds_read_b128 v[34:37], v162
	s_waitcnt lgkmcnt(3)
	global_store_dwordx4 v[150:151], v[10:13], off offset:1536 nt
	s_waitcnt lgkmcnt(2)
	global_store_dwordx4 v[152:153], v[18:21], off offset:1536 nt
	s_waitcnt lgkmcnt(1)
	global_store_dwordx4 v[160:161], v[26:29], off offset:1536 nt
	s_waitcnt lgkmcnt(0)
	global_store_dwordx4 v[164:165], v[34:37], off offset:1536 nt
	s_waitcnt vmcnt(23)
	v_mul_f32_e32 v2, 0x43800000, v6
	s_waitcnt vmcnt(22)
	v_mul_f32_e32 v3, 0x43800000, v14
	v_med3_f32 v2, v2, s0, v1
	v_med3_f32 v3, v3, s0, v1
	v_mov_b32_e32 v10, v5
	v_cvt_pk_fp8_f32 v10, v2, v3
	s_waitcnt vmcnt(21)
	v_mul_f32_e32 v4, 0x43800000, v30
	s_waitcnt vmcnt(20)
	v_mul_f32_e32 v2, 0x43800000, v22
	v_med3_f32 v3, v4, s0, v1
	v_med3_f32 v2, v2, s0, v1
	v_cvt_pk_fp8_f32 v10, v3, v2 op_sel:[0,0,1]
	s_waitcnt vmcnt(19)
	v_mul_f32_e32 v2, 0x43800000, v42
	s_waitcnt vmcnt(18)
	v_mul_f32_e32 v3, 0x43800000, v46
	v_med3_f32 v2, v2, s0, v1
	v_med3_f32 v3, v3, s0, v1
	v_mov_b32_e32 v11, v5
	v_cvt_pk_fp8_f32 v11, v2, v3
	s_waitcnt vmcnt(17)
	v_mul_f32_e32 v4, 0x43800000, v62
	s_waitcnt vmcnt(16)
	v_mul_f32_e32 v2, 0x43800000, v54
	v_med3_f32 v3, v4, s0, v1
	v_med3_f32 v2, v2, s0, v1
	v_cvt_pk_fp8_f32 v11, v3, v2 op_sel:[0,0,1]
	s_waitcnt vmcnt(15)
	v_mul_f32_e32 v2, 0x43800000, v74
	s_waitcnt vmcnt(14)
	v_mul_f32_e32 v3, 0x43800000, v78
	v_med3_f32 v2, v2, s0, v1
	v_med3_f32 v3, v3, s0, v1
	v_mov_b32_e32 v12, v5
	v_cvt_pk_fp8_f32 v12, v2, v3
	s_waitcnt vmcnt(13)
	v_mul_f32_e32 v4, 0x43800000, v102
	s_waitcnt vmcnt(12)
	v_mul_f32_e32 v2, 0x43800000, v86
	v_med3_f32 v3, v4, s0, v1
	v_med3_f32 v2, v2, s0, v1
	v_cvt_pk_fp8_f32 v12, v3, v2 op_sel:[0,0,1]
	s_waitcnt vmcnt(11)
	v_mul_f32_e32 v2, 0x43800000, v106
	s_waitcnt vmcnt(10)
	v_mul_f32_e32 v3, 0x43800000, v114
	v_med3_f32 v2, v2, s0, v1
	v_med3_f32 v3, v3, s0, v1
	v_mov_b32_e32 v13, v5
	v_cvt_pk_fp8_f32 v13, v2, v3
	s_waitcnt vmcnt(9)
	v_mul_f32_e32 v4, 0x43800000, v130
	s_waitcnt vmcnt(8)
	v_mul_f32_e32 v2, 0x43800000, v122
	v_med3_f32 v3, v4, s0, v1
	v_med3_f32 v2, v2, s0, v1
	v_cvt_pk_fp8_f32 v13, v3, v2 op_sel:[0,0,1]
	v_mul_f32_e32 v2, 0x43800000, v7
	v_mul_f32_e32 v3, 0x43800000, v15
	v_med3_f32 v2, v2, s0, v1
	v_med3_f32 v3, v3, s0, v1
	v_mov_b32_e32 v18, v5
	v_cvt_pk_fp8_f32 v18, v2, v3
	v_mul_f32_e32 v4, 0x43800000, v31
	v_mul_f32_e32 v2, 0x43800000, v23
	v_med3_f32 v3, v4, s0, v1
	v_med3_f32 v2, v2, s0, v1
	v_cvt_pk_fp8_f32 v18, v3, v2 op_sel:[0,0,1]
	v_mul_f32_e32 v2, 0x43800000, v43
	v_mul_f32_e32 v3, 0x43800000, v47
	v_med3_f32 v2, v2, s0, v1
	v_med3_f32 v3, v3, s0, v1
	v_mov_b32_e32 v19, v5
	v_cvt_pk_fp8_f32 v19, v2, v3
	v_mul_f32_e32 v4, 0x43800000, v63
	v_mul_f32_e32 v2, 0x43800000, v55
	v_med3_f32 v3, v4, s0, v1
	v_med3_f32 v2, v2, s0, v1
	v_cvt_pk_fp8_f32 v19, v3, v2 op_sel:[0,0,1]
	v_mul_f32_e32 v2, 0x43800000, v75
	v_mul_f32_e32 v3, 0x43800000, v79
	v_med3_f32 v2, v2, s0, v1
	v_med3_f32 v3, v3, s0, v1
	v_mov_b32_e32 v20, v5
	v_cvt_pk_fp8_f32 v20, v2, v3
	v_mul_f32_e32 v4, 0x43800000, v103
	v_mul_f32_e32 v2, 0x43800000, v87
	v_med3_f32 v3, v4, s0, v1
	v_med3_f32 v2, v2, s0, v1
	v_cvt_pk_fp8_f32 v20, v3, v2 op_sel:[0,0,1]
	v_mul_f32_e32 v2, 0x43800000, v107
	v_mul_f32_e32 v3, 0x43800000, v115
	v_med3_f32 v2, v2, s0, v1
	v_med3_f32 v3, v3, s0, v1
	v_mov_b32_e32 v21, v5
	v_cvt_pk_fp8_f32 v21, v2, v3
	v_mul_f32_e32 v4, 0x43800000, v131
	v_mul_f32_e32 v2, 0x43800000, v123
	v_med3_f32 v3, v4, s0, v1
	v_med3_f32 v2, v2, s0, v1
	v_cvt_pk_fp8_f32 v21, v3, v2 op_sel:[0,0,1]
	v_mul_f32_e32 v2, 0x43800000, v8
	v_mul_f32_e32 v3, 0x43800000, v16
	v_med3_f32 v2, v2, s0, v1
	v_med3_f32 v3, v3, s0, v1
	v_mov_b32_e32 v26, v5
	v_cvt_pk_fp8_f32 v26, v2, v3
	v_mul_f32_e32 v4, 0x43800000, v32
	v_mul_f32_e32 v2, 0x43800000, v24
	v_med3_f32 v3, v4, s0, v1
	v_med3_f32 v2, v2, s0, v1
	v_cvt_pk_fp8_f32 v26, v3, v2 op_sel:[0,0,1]
	v_mul_f32_e32 v2, 0x43800000, v44
	v_mul_f32_e32 v3, 0x43800000, v48
	v_med3_f32 v2, v2, s0, v1
	v_med3_f32 v3, v3, s0, v1
	v_mov_b32_e32 v27, v5
	v_cvt_pk_fp8_f32 v27, v2, v3
	v_mul_f32_e32 v4, 0x43800000, v64
	v_mul_f32_e32 v2, 0x43800000, v56
	v_med3_f32 v3, v4, s0, v1
	v_med3_f32 v2, v2, s0, v1
	v_cvt_pk_fp8_f32 v27, v3, v2 op_sel:[0,0,1]
	v_mul_f32_e32 v2, 0x43800000, v76
	v_mul_f32_e32 v3, 0x43800000, v80
	v_med3_f32 v2, v2, s0, v1
	v_med3_f32 v3, v3, s0, v1
	v_mov_b32_e32 v28, v5
	v_cvt_pk_fp8_f32 v28, v2, v3
	v_mul_f32_e32 v4, 0x43800000, v104
	v_mul_f32_e32 v2, 0x43800000, v88
	v_med3_f32 v3, v4, s0, v1
	v_med3_f32 v2, v2, s0, v1
	v_cvt_pk_fp8_f32 v28, v3, v2 op_sel:[0,0,1]
	v_mul_f32_e32 v2, 0x43800000, v108
	v_mul_f32_e32 v3, 0x43800000, v116
	v_med3_f32 v2, v2, s0, v1
	v_med3_f32 v3, v3, s0, v1
	v_mov_b32_e32 v29, v5
	v_cvt_pk_fp8_f32 v29, v2, v3
	v_mul_f32_e32 v4, 0x43800000, v132
	v_mul_f32_e32 v2, 0x43800000, v124
	v_med3_f32 v3, v4, s0, v1
	v_med3_f32 v2, v2, s0, v1
	v_cvt_pk_fp8_f32 v29, v3, v2 op_sel:[0,0,1]
	v_mul_f32_e32 v2, 0x43800000, v9
	v_mul_f32_e32 v3, 0x43800000, v17
	v_med3_f32 v6, v2, s0, v1
	v_med3_f32 v3, v3, s0, v1
	v_mov_b32_e32 v2, v5
	v_cvt_pk_fp8_f32 v2, v6, v3
	v_mul_f32_e32 v4, 0x43800000, v33
	v_mul_f32_e32 v3, 0x43800000, v25
	v_med3_f32 v4, v4, s0, v1
	v_med3_f32 v3, v3, s0, v1
	v_cvt_pk_fp8_f32 v2, v4, v3 op_sel:[0,0,1]
	v_mul_f32_e32 v3, 0x43800000, v45
	v_mul_f32_e32 v4, 0x43800000, v49
	v_med3_f32 v7, v3, s0, v1
	v_med3_f32 v4, v4, s0, v1
	v_mov_b32_e32 v3, v5
	v_cvt_pk_fp8_f32 v3, v7, v4
	v_mul_f32_e32 v6, 0x43800000, v65
	v_mul_f32_e32 v4, 0x43800000, v57
	v_med3_f32 v6, v6, s0, v1
	v_med3_f32 v4, v4, s0, v1
	v_cvt_pk_fp8_f32 v3, v6, v4 op_sel:[0,0,1]
	v_mul_f32_e32 v4, 0x43800000, v77
	v_mul_f32_e32 v6, 0x43800000, v81
	v_med3_f32 v8, v4, s0, v1
	v_med3_f32 v6, v6, s0, v1
	v_mov_b32_e32 v4, v5
	v_cvt_pk_fp8_f32 v4, v8, v6
	v_mul_f32_e32 v7, 0x43800000, v105
	v_mul_f32_e32 v6, 0x43800000, v89
	v_med3_f32 v7, v7, s0, v1
	v_med3_f32 v6, v6, s0, v1
	v_cvt_pk_fp8_f32 v4, v7, v6 op_sel:[0,0,1]
	v_mul_f32_e32 v6, 0x43800000, v109
	v_mul_f32_e32 v7, 0x43800000, v117
	v_med3_f32 v6, v6, s0, v1
	v_med3_f32 v7, v7, s0, v1
	v_cvt_pk_fp8_f32 v5, v6, v7
	v_mul_f32_e32 v8, 0x43800000, v133
	v_mul_f32_e32 v6, 0x43800000, v125
	v_med3_f32 v7, v8, s0, v1
	v_med3_f32 v1, v6, s0, v1
	v_cvt_pk_fp8_f32 v5, v7, v1 op_sel:[0,0,1]
	ds_write_b128 v166, v[10:13] offset:34816
	ds_write_b128 v166, v[18:21] offset:35088
	ds_write_b128 v166, v[26:29] offset:35360
	ds_write_b128 v166, v[2:5] offset:35632
	s_waitcnt lgkmcnt(0)
	s_barrier
	ds_read_b128 v[2:5], v154 offset:34816
	ds_read_b128 v[6:9], v156 offset:34816
	ds_read_b128 v[10:13], v158 offset:34816
	ds_read_b128 v[14:17], v162 offset:34816
	s_waitcnt lgkmcnt(3)
	global_store_dwordx4 v[150:151], v[2:5], off offset:1792 nt
	s_waitcnt lgkmcnt(2)
	global_store_dwordx4 v[152:153], v[6:9], off offset:1792 nt
	s_waitcnt lgkmcnt(1)
	global_store_dwordx4 v[160:161], v[10:13], off offset:1792 nt
	s_waitcnt lgkmcnt(0)
	global_store_dwordx4 v[164:165], v[14:17], off offset:1792 nt
	s_barrier

.LBB0_1242:
	v_readlane_b32 s2, v254, 61
	v_readlane_b32 s3, v254, 62
	s_and_b64 vcc, exec, s[2:3]
	s_cbranch_vccnz .LBB0_1246
	s_add_i32 s2, s74, s99
	v_readlane_b32 s20, v254, 4
	s_ashr_i32 s4, s2, 4
	v_readlane_b32 s21, v254, 5
	v_readlane_b32 s22, v254, 6
	v_readlane_b32 s23, v254, 7
	v_readlane_b32 s24, v254, 8
	v_readlane_b32 s25, v254, 9
	s_ashr_i32 s5, s4, 31
	v_readlane_b32 s26, v254, 10
	v_readlane_b32 s27, v254, 11
	s_mov_b64 s[20:21], s[24:25]
	s_lshl_b64 s[2:3], s[4:5], 24
	s_mov_b64 s[22:23], s[26:27]
	s_add_u32 s2, s22, s2
	s_addc_u32 s3, s23, s3
	s_lshl_b32 s6, s74, 7
	s_and_b32 s9, s6, 0x780
	s_lshl_b32 s6, s9, 2
	s_add_u32 s6, s2, s6
	s_addc_u32 s7, s3, 0
	s_lshl_b64 s[2:3], s[4:5], 22
	s_lshl_b32 s5, s9, 11
	s_add_u32 s2, s78, s2
	v_mov_b32_e32 v134, v0
	s_addc_u32 s3, s79, s3
	s_add_u32 s2, s2, s5
	v_readfirstlane_b32 s8, v134
	s_addc_u32 s3, s3, 0
	s_ashr_i32 s5, s8, 1
	v_lshrrev_b32_e32 v1, 1, v134
	s_andn2_b32 s5, s5, 31
	v_and_b32_e32 v135, 16, v1
	v_or_b32_e32 v2, s5, v135
	v_ashrrev_i32_e32 v3, 31, v2
	v_lshlrev_b32_e32 v1, 2, v134
	v_lshlrev_b64 v[2:3], 13, v[2:3]
	v_and_b32_e32 v140, 0x7c, v1
	v_lshl_add_u64 v[2:3], s[6:7], 0, v[2:3]
	v_lshlrev_b32_e32 v4, 2, v140
	v_mov_b32_e32 v5, 0
	v_lshl_add_u64 v[2:3], v[2:3], 0, v[4:5]
	s_movk_i32 s6, 0x2000
	v_add_co_u32_e32 v6, vcc, s6, v2
	s_movk_i32 s6, 0x4000
	s_nop 0
	v_addc_co_u32_e32 v7, vcc, 0, v3, vcc
	global_load_dwordx4 v[30:33], v[2:3], off sc0 nt
	global_load_dwordx4 v[38:41], v[6:7], off sc0 nt
	v_add_co_u32_e32 v6, vcc, s6, v2
	s_movk_i32 s6, 0x6000
	s_nop 0
	v_addc_co_u32_e32 v7, vcc, 0, v3, vcc
	v_add_co_u32_e32 v8, vcc, s6, v2
	s_mov_b32 s6, 0x8000
	s_nop 0
	v_addc_co_u32_e32 v9, vcc, 0, v3, vcc
	global_load_dwordx4 v[58:61], v[6:7], off sc0 nt
	global_load_dwordx4 v[46:49], v[8:9], off sc0 nt
	v_add_co_u32_e32 v6, vcc, s6, v2
	s_mov_b32 s6, 0xa000
	s_nop 0
	v_addc_co_u32_e32 v7, vcc, 0, v3, vcc
	v_add_co_u32_e32 v8, vcc, s6, v2
	s_mov_b32 s6, 0xc000
	s_nop 0
	v_addc_co_u32_e32 v9, vcc, 0, v3, vcc
	global_load_dwordx4 v[62:65], v[6:7], off sc0 nt
	global_load_dwordx4 v[66:69], v[8:9], off sc0 nt
	v_add_co_u32_e32 v6, vcc, s6, v2
	s_mov_b32 s6, 0xe000
	s_nop 0
	v_addc_co_u32_e32 v7, vcc, 0, v3, vcc
	v_add_co_u32_e32 v8, vcc, s6, v2
	s_mov_b32 s6, 0x10000
	s_nop 0
	v_addc_co_u32_e32 v9, vcc, 0, v3, vcc
	global_load_dwordx4 v[90:93], v[6:7], off sc0 nt
	global_load_dwordx4 v[78:81], v[8:9], off sc0 nt
	v_add_co_u32_e32 v6, vcc, s6, v2
	s_mov_b32 s6, 0x12000
	s_nop 0
	v_addc_co_u32_e32 v7, vcc, 0, v3, vcc
	v_add_co_u32_e32 v8, vcc, s6, v2
	s_mov_b32 s6, 0x14000
	s_nop 0
	v_addc_co_u32_e32 v9, vcc, 0, v3, vcc
	global_load_dwordx4 v[94:97], v[6:7], off sc0 nt
	global_load_dwordx4 v[102:105], v[8:9], off sc0 nt
	v_add_co_u32_e32 v6, vcc, s6, v2
	s_mov_b32 s6, 0x16000
	s_nop 0
	v_addc_co_u32_e32 v7, vcc, 0, v3, vcc
	v_add_co_u32_e32 v8, vcc, s6, v2
	s_mov_b32 s6, 0x18000
	s_nop 0
	v_addc_co_u32_e32 v9, vcc, 0, v3, vcc
	global_load_dwordx4 v[114:117], v[6:7], off sc0 nt
	global_load_dwordx4 v[110:113], v[8:9], off sc0 nt
	v_add_co_u32_e32 v6, vcc, s6, v2
	s_mov_b32 s6, 0x1a000
	s_nop 0
	v_addc_co_u32_e32 v7, vcc, 0, v3, vcc
	v_add_co_u32_e32 v8, vcc, s6, v2
	s_mov_b32 s6, 0x1c000
	s_nop 0
	v_addc_co_u32_e32 v9, vcc, 0, v3, vcc
	global_load_dwordx4 v[118:121], v[6:7], off sc0 nt
	global_load_dwordx4 v[122:125], v[8:9], off sc0 nt
	v_add_co_u32_e32 v6, vcc, s6, v2
	s_mov_b32 s6, 0x1e000
	s_nop 0
	v_addc_co_u32_e32 v7, vcc, 0, v3, vcc
	v_add_co_u32_e32 v8, vcc, s6, v2
	s_mov_b32 s6, 0x200000
	s_nop 0
	v_addc_co_u32_e32 v9, vcc, 0, v3, vcc
	v_add_co_u32_e32 v14, vcc, s6, v2
	s_mov_b32 s6, 0x202000
	s_nop 0
	v_addc_co_u32_e32 v15, vcc, 0, v3, vcc
	v_add_co_u32_e32 v16, vcc, s6, v2
	s_mov_b32 s6, 0x204000
	s_nop 0
	v_addc_co_u32_e32 v17, vcc, 0, v3, vcc
	v_add_co_u32_e32 v22, vcc, s6, v2
	s_mov_b32 s6, 0x206000
	s_nop 0
	v_addc_co_u32_e32 v23, vcc, 0, v3, vcc
	v_add_co_u32_e32 v24, vcc, s6, v2
	s_mov_b32 s6, 0x208000
	s_nop 0
	v_addc_co_u32_e32 v25, vcc, 0, v3, vcc
	v_add_co_u32_e32 v34, vcc, s6, v2
	s_mov_b32 s6, 0x20a000
	s_nop 0
	v_addc_co_u32_e32 v35, vcc, 0, v3, vcc
	v_add_co_u32_e32 v36, vcc, s6, v2
	s_mov_b32 s6, 0x20c000
	s_nop 0
	v_addc_co_u32_e32 v37, vcc, 0, v3, vcc
	v_add_co_u32_e32 v50, vcc, s6, v2
	s_mov_b32 s6, 0x20e000
	s_nop 0
	v_addc_co_u32_e32 v51, vcc, 0, v3, vcc
	v_add_co_u32_e32 v52, vcc, s6, v2
	s_mov_b32 s6, 0x210000
	s_nop 0
	v_addc_co_u32_e32 v53, vcc, 0, v3, vcc
	v_add_co_u32_e32 v70, vcc, s6, v2
	s_mov_b32 s6, 0x212000
	s_nop 0
	v_addc_co_u32_e32 v71, vcc, 0, v3, vcc
	v_add_co_u32_e32 v72, vcc, s6, v2
	s_mov_b32 s6, 0x214000
	s_nop 0
	v_addc_co_u32_e32 v73, vcc, 0, v3, vcc
	v_add_co_u32_e32 v82, vcc, s6, v2
	s_mov_b32 s6, 0x216000
	s_nop 0
	v_addc_co_u32_e32 v83, vcc, 0, v3, vcc
	v_add_co_u32_e32 v84, vcc, s6, v2
	s_mov_b32 s6, 0x218000
	s_nop 0
	v_addc_co_u32_e32 v85, vcc, 0, v3, vcc
	global_load_dwordx4 v[130:133], v[6:7], off sc0 nt
	global_load_dwordx4 v[126:129], v[8:9], off sc0 nt
	s_nop 0
	global_load_dwordx4 v[6:9], v[14:15], off sc0 nt
	global_load_dwordx4 v[10:13], v[16:17], off sc0 nt
	global_load_dwordx4 v[18:21], v[22:23], off sc0 nt
	s_nop 0
	global_load_dwordx4 v[14:17], v[24:25], off sc0 nt
	s_nop 0
	global_load_dwordx4 v[22:25], v[34:35], off sc0 nt
	global_load_dwordx4 v[26:29], v[36:37], off sc0 nt
	global_load_dwordx4 v[42:45], v[50:51], off sc0 nt
	s_nop 0
	global_load_dwordx4 v[34:37], v[52:53], off sc0 nt
	s_nop 0
	global_load_dwordx4 v[50:53], v[70:71], off sc0 nt
	global_load_dwordx4 v[54:57], v[72:73], off sc0 nt
	global_load_dwordx4 v[74:77], v[82:83], off sc0 nt
	s_nop 0
	global_load_dwordx4 v[70:73], v[84:85], off sc0 nt
	v_add_co_u32_e32 v82, vcc, s6, v2
	s_mov_b32 s6, 0x21a000
	s_nop 0
	v_addc_co_u32_e32 v83, vcc, 0, v3, vcc
	v_add_co_u32_e32 v86, vcc, s6, v2
	s_mov_b32 s6, 0x21c000
	s_nop 0
	v_addc_co_u32_e32 v87, vcc, 0, v3, vcc
	v_add_co_u32_e32 v98, vcc, s6, v2
	s_mov_b32 s6, 0x21e000
	s_nop 0
	v_addc_co_u32_e32 v99, vcc, 0, v3, vcc
	v_add_co_u32_e32 v100, vcc, s6, v2
	global_load_dwordx4 v[82:85], v[82:83], off sc0 nt
	s_nop 0
	global_load_dwordx4 v[86:89], v[86:87], off sc0 nt
	v_addc_co_u32_e32 v101, vcc, 0, v3, vcc
	global_load_dwordx4 v[106:109], v[98:99], off sc0 nt
	s_nop 0
	global_load_dwordx4 v[98:101], v[100:101], off sc0 nt
	s_add_i32 s7, s5, 0
	s_waitcnt vmcnt(0)
	v_mul_f32_e32 v4, 0x43800000, v30
	v_mul_f32_e32 v30, 0x43800000, v38
	s_mov_b32 s5, 0xc3e00000
	v_mov_b32_e32 v1, 0x43e00000
	v_med3_f32 v4, v4, s5, v1
	v_med3_f32 v30, v30, s5, v1
	v_mov_b32_e32 v136, v5
	v_cvt_pk_fp8_f32 v136, v4, v30
	v_mul_f32_e32 v38, 0x43800000, v58
	v_mul_f32_e32 v4, 0x43800000, v46
	v_med3_f32 v30, v38, s5, v1
	v_med3_f32 v4, v4, s5, v1
	v_cvt_pk_fp8_f32 v136, v30, v4 op_sel:[0,0,1]
	v_mul_f32_e32 v4, 0x43800000, v62
	v_mul_f32_e32 v30, 0x43800000, v66
	v_med3_f32 v4, v4, s5, v1
	v_med3_f32 v30, v30, s5, v1
	v_mov_b32_e32 v137, v5
	v_cvt_pk_fp8_f32 v137, v4, v30
	v_mul_f32_e32 v38, 0x43800000, v90
	v_mul_f32_e32 v4, 0x43800000, v78
	v_med3_f32 v30, v38, s5, v1
	v_med3_f32 v4, v4, s5, v1
	v_cvt_pk_fp8_f32 v137, v30, v4 op_sel:[0,0,1]
	v_mul_f32_e32 v4, 0x43800000, v94
	v_mul_f32_e32 v30, 0x43800000, v102
	v_med3_f32 v4, v4, s5, v1
	v_med3_f32 v30, v30, s5, v1
	v_mov_b32_e32 v138, v5
	v_cvt_pk_fp8_f32 v138, v4, v30
	v_mul_f32_e32 v38, 0x43800000, v114
	v_mul_f32_e32 v4, 0x43800000, v110
	v_med3_f32 v30, v38, s5, v1
	v_med3_f32 v4, v4, s5, v1
	v_cvt_pk_fp8_f32 v138, v30, v4 op_sel:[0,0,1]
	v_mul_f32_e32 v4, 0x43800000, v118
	v_mul_f32_e32 v30, 0x43800000, v122
	v_med3_f32 v4, v4, s5, v1
	v_med3_f32 v30, v30, s5, v1
	v_mov_b32_e32 v139, v5
	v_cvt_pk_fp8_f32 v139, v4, v30
	v_mul_f32_e32 v38, 0x43800000, v130
	v_mul_f32_e32 v4, 0x43800000, v126
	v_med3_f32 v30, v38, s5, v1
	v_med3_f32 v4, v4, s5, v1
	v_cvt_pk_fp8_f32 v139, v30, v4 op_sel:[0,0,1]
	v_mul_u32_u24_e32 v4, 0x110, v140
	v_add3_u32 v168, s7, v135, v4
	v_mul_f32_e32 v4, 0x43800000, v31
	v_mul_f32_e32 v30, 0x43800000, v39
	v_med3_f32 v4, v4, s5, v1
	v_med3_f32 v30, v30, s5, v1
	v_mov_b32_e32 v140, v5
	v_cvt_pk_fp8_f32 v140, v4, v30
	v_mul_f32_e32 v31, 0x43800000, v59
	v_mul_f32_e32 v4, 0x43800000, v47
	v_med3_f32 v30, v31, s5, v1
	v_med3_f32 v4, v4, s5, v1
	v_cvt_pk_fp8_f32 v140, v30, v4 op_sel:[0,0,1]
	v_mul_f32_e32 v4, 0x43800000, v63
	v_mul_f32_e32 v30, 0x43800000, v67
	v_med3_f32 v4, v4, s5, v1
	v_med3_f32 v30, v30, s5, v1
	v_mov_b32_e32 v141, v5
	v_cvt_pk_fp8_f32 v141, v4, v30
	v_mul_f32_e32 v31, 0x43800000, v91
	v_mul_f32_e32 v4, 0x43800000, v79
	v_med3_f32 v30, v31, s5, v1
	v_med3_f32 v4, v4, s5, v1
	v_cvt_pk_fp8_f32 v141, v30, v4 op_sel:[0,0,1]
	v_mul_f32_e32 v4, 0x43800000, v95
	v_mul_f32_e32 v30, 0x43800000, v103
	v_med3_f32 v4, v4, s5, v1
	v_med3_f32 v30, v30, s5, v1
	v_mov_b32_e32 v142, v5
	v_cvt_pk_fp8_f32 v142, v4, v30
	v_mul_f32_e32 v31, 0x43800000, v115
	v_mul_f32_e32 v4, 0x43800000, v111
	v_med3_f32 v30, v31, s5, v1
	v_med3_f32 v4, v4, s5, v1
	v_cvt_pk_fp8_f32 v142, v30, v4 op_sel:[0,0,1]
	v_mul_f32_e32 v4, 0x43800000, v119
	v_mul_f32_e32 v30, 0x43800000, v123
	v_med3_f32 v4, v4, s5, v1
	v_med3_f32 v30, v30, s5, v1
	v_mov_b32_e32 v143, v5
	v_cvt_pk_fp8_f32 v143, v4, v30
	v_mul_f32_e32 v31, 0x43800000, v131
	v_mul_f32_e32 v4, 0x43800000, v127
	v_med3_f32 v30, v31, s5, v1
	v_med3_f32 v4, v4, s5, v1
	v_cvt_pk_fp8_f32 v143, v30, v4 op_sel:[0,0,1]
	v_mul_f32_e32 v4, 0x43800000, v32
	v_mul_f32_e32 v30, 0x43800000, v40
	v_med3_f32 v4, v4, s5, v1
	v_med3_f32 v30, v30, s5, v1
	v_mov_b32_e32 v144, v5
	v_cvt_pk_fp8_f32 v144, v4, v30
	v_mul_f32_e32 v31, 0x43800000, v60
	v_mul_f32_e32 v4, 0x43800000, v48
	v_med3_f32 v30, v31, s5, v1
	v_med3_f32 v4, v4, s5, v1
	v_cvt_pk_fp8_f32 v144, v30, v4 op_sel:[0,0,1]
	v_mul_f32_e32 v4, 0x43800000, v64
	v_mul_f32_e32 v30, 0x43800000, v68
	v_med3_f32 v4, v4, s5, v1
	v_med3_f32 v30, v30, s5, v1
	v_mov_b32_e32 v145, v5
	v_cvt_pk_fp8_f32 v145, v4, v30
	v_mul_f32_e32 v31, 0x43800000, v92
	v_mul_f32_e32 v4, 0x43800000, v80
	v_med3_f32 v30, v31, s5, v1
	v_med3_f32 v4, v4, s5, v1
	v_cvt_pk_fp8_f32 v145, v30, v4 op_sel:[0,0,1]
	v_mul_f32_e32 v4, 0x43800000, v96
	v_mul_f32_e32 v30, 0x43800000, v104
	v_med3_f32 v4, v4, s5, v1
	v_med3_f32 v30, v30, s5, v1
	v_mov_b32_e32 v146, v5
	v_cvt_pk_fp8_f32 v146, v4, v30
	v_mul_f32_e32 v31, 0x43800000, v116
	v_mul_f32_e32 v4, 0x43800000, v112
	v_med3_f32 v30, v31, s5, v1
	v_med3_f32 v4, v4, s5, v1
	v_cvt_pk_fp8_f32 v146, v30, v4 op_sel:[0,0,1]
	v_mul_f32_e32 v4, 0x43800000, v120
	v_mul_f32_e32 v30, 0x43800000, v124
	v_med3_f32 v4, v4, s5, v1
	v_med3_f32 v30, v30, s5, v1
	v_mov_b32_e32 v147, v5
	v_cvt_pk_fp8_f32 v147, v4, v30
	v_mul_f32_e32 v31, 0x43800000, v132
	v_mul_f32_e32 v4, 0x43800000, v128
	v_med3_f32 v30, v31, s5, v1
	v_med3_f32 v4, v4, s5, v1
	v_cvt_pk_fp8_f32 v147, v30, v4 op_sel:[0,0,1]
	v_mul_f32_e32 v4, 0x43800000, v33
	v_mul_f32_e32 v30, 0x43800000, v41
	v_med3_f32 v4, v4, s5, v1
	v_med3_f32 v32, v30, s5, v1
	v_mov_b32_e32 v30, v5
	v_cvt_pk_fp8_f32 v30, v4, v32
	v_mul_f32_e32 v31, 0x43800000, v61
	v_mul_f32_e32 v4, 0x43800000, v49
	v_med3_f32 v31, v31, s5, v1
	v_med3_f32 v4, v4, s5, v1
	v_cvt_pk_fp8_f32 v30, v31, v4 op_sel:[0,0,1]
	v_mul_f32_e32 v4, 0x43800000, v65
	v_mul_f32_e32 v31, 0x43800000, v69
	v_med3_f32 v4, v4, s5, v1
	v_med3_f32 v33, v31, s5, v1
	v_mov_b32_e32 v31, v5
	v_cvt_pk_fp8_f32 v31, v4, v33
	v_mul_f32_e32 v32, 0x43800000, v93
	v_mul_f32_e32 v4, 0x43800000, v81
	v_med3_f32 v32, v32, s5, v1
	v_med3_f32 v4, v4, s5, v1
	v_cvt_pk_fp8_f32 v31, v32, v4 op_sel:[0,0,1]
	v_mul_f32_e32 v4, 0x43800000, v97
	v_mul_f32_e32 v32, 0x43800000, v105
	v_med3_f32 v4, v4, s5, v1
	v_med3_f32 v38, v32, s5, v1
	v_mov_b32_e32 v32, v5
	v_cvt_pk_fp8_f32 v32, v4, v38
	v_mul_f32_e32 v33, 0x43800000, v117
	v_mul_f32_e32 v4, 0x43800000, v113
	v_med3_f32 v33, v33, s5, v1
	v_med3_f32 v4, v4, s5, v1
	v_cvt_pk_fp8_f32 v32, v33, v4 op_sel:[0,0,1]
	v_mul_f32_e32 v4, 0x43800000, v121
	v_mul_f32_e32 v33, 0x43800000, v125
	v_med3_f32 v4, v4, s5, v1
	v_med3_f32 v39, v33, s5, v1
	v_mov_b32_e32 v33, v5
	v_cvt_pk_fp8_f32 v33, v4, v39
	v_mul_f32_e32 v38, 0x43800000, v133
	v_mul_f32_e32 v4, 0x43800000, v129
	v_med3_f32 v38, v38, s5, v1
	v_med3_f32 v4, v4, s5, v1
	v_cvt_pk_fp8_f32 v33, v38, v4 op_sel:[0,0,1]
	ds_write_b128 v168, v[136:139]
	ds_write_b128 v168, v[140:143] offset:272
	ds_write_b128 v168, v[144:147] offset:544
	ds_write_b128 v168, v[30:33] offset:816
	v_add_u32_e32 v30, 0x200, v134
	v_ashrrev_i32_e32 v136, 4, v30
	v_add_u32_e32 v30, 0x400, v134
	v_ashrrev_i32_e32 v142, 4, v30
	v_add_u32_e32 v30, 0x600, v134
	v_lshlrev_b32_e32 v4, 4, v134
	v_ashrrev_i32_e32 v130, 4, v134
	v_ashrrev_i32_e32 v134, 4, v30
	v_ashrrev_i32_e32 v131, 31, v130
	v_ashrrev_i32_e32 v137, 31, v136
	v_ashrrev_i32_e32 v143, 31, v142
	v_ashrrev_i32_e32 v135, 31, v134
	s_movk_i32 s6, 0x110
	s_waitcnt lgkmcnt(0)
	s_barrier
	v_and_b32_e32 v4, 0xf0, v4
	v_lshlrev_b64 v[150:151], 11, v[130:131]
	v_lshlrev_b64 v[152:153], 11, v[136:137]
	v_lshlrev_b64 v[154:155], 11, v[142:143]
	v_lshlrev_b64 v[156:157], 11, v[134:135]
	s_mov_b32 s7, 0x400000
	v_add_co_u32_e32 v30, vcc, s7, v2
	s_mov_b32 s7, 0x402000
	s_nop 0
	v_addc_co_u32_e32 v31, vcc, 0, v3, vcc
	v_add_co_u32_e32 v38, vcc, s7, v2
	s_mov_b32 s7, 0x404000
	s_nop 0
	v_addc_co_u32_e32 v39, vcc, 0, v3, vcc
	v_add_co_u32_e32 v62, vcc, s7, v2
	s_mov_b32 s7, 0x406000
	s_nop 0
	v_addc_co_u32_e32 v63, vcc, 0, v3, vcc
	v_add_co_u32_e32 v64, vcc, s7, v2
	s_mov_b32 s7, 0x408000
	s_nop 0
	v_addc_co_u32_e32 v65, vcc, 0, v3, vcc
	v_add_co_u32_e32 v78, vcc, s7, v2
	s_mov_b32 s7, 0x40a000
	s_nop 0
	v_addc_co_u32_e32 v79, vcc, 0, v3, vcc
	v_add_co_u32_e32 v80, vcc, s7, v2
	s_mov_b32 s7, 0x40c000
	s_nop 0
	v_addc_co_u32_e32 v81, vcc, 0, v3, vcc
	v_add_co_u32_e32 v94, vcc, s7, v2
	s_mov_b32 s7, 0x40e000
	s_nop 0
	v_addc_co_u32_e32 v95, vcc, 0, v3, vcc
	v_add_co_u32_e32 v96, vcc, s7, v2
	s_mov_b32 s7, 0x410000
	s_nop 0
	v_addc_co_u32_e32 v97, vcc, 0, v3, vcc
	v_add_co_u32_e32 v110, vcc, s7, v2
	s_mov_b32 s7, 0x412000
	s_nop 0
	v_addc_co_u32_e32 v111, vcc, 0, v3, vcc
	v_add_co_u32_e32 v112, vcc, s7, v2
	s_mov_b32 s7, 0x414000
	s_nop 0
	v_addc_co_u32_e32 v113, vcc, 0, v3, vcc
	global_load_dwordx4 v[30:33], v[30:31], off sc0 nt
	s_nop 0
	global_load_dwordx4 v[38:41], v[38:39], off sc0 nt
	s_nop 0
	global_load_dwordx4 v[58:61], v[62:63], off sc0 nt
	global_load_dwordx4 v[46:49], v[64:65], off sc0 nt
	s_nop 0
	global_load_dwordx4 v[62:65], v[78:79], off sc0 nt
	global_load_dwordx4 v[66:69], v[80:81], off sc0 nt
	global_load_dwordx4 v[90:93], v[94:95], off sc0 nt
	s_nop 0
	global_load_dwordx4 v[78:81], v[96:97], off sc0 nt
	s_nop 0
	global_load_dwordx4 v[94:97], v[110:111], off sc0 nt
	global_load_dwordx4 v[102:105], v[112:113], off sc0 nt
	v_add_co_u32_e32 v110, vcc, s7, v2
	s_mov_b32 s7, 0x416000
	s_nop 0
	v_addc_co_u32_e32 v111, vcc, 0, v3, vcc
	v_add_co_u32_e32 v112, vcc, s7, v2
	s_mov_b32 s7, 0x418000
	s_nop 0
	v_addc_co_u32_e32 v113, vcc, 0, v3, vcc
	v_add_co_u32_e32 v118, vcc, s7, v2
	s_mov_b32 s7, 0x41a000
	s_nop 0
	v_addc_co_u32_e32 v119, vcc, 0, v3, vcc
	v_add_co_u32_e32 v122, vcc, s7, v2
	s_mov_b32 s7, 0x41c000
	s_nop 0
	v_addc_co_u32_e32 v123, vcc, 0, v3, vcc
	v_add_co_u32_e32 v126, vcc, s7, v2
	s_mov_b32 s7, 0x41e000
	s_nop 0
	v_addc_co_u32_e32 v127, vcc, 0, v3, vcc
	v_add_co_u32_e32 v128, vcc, s7, v2
	global_load_dwordx4 v[114:117], v[110:111], off sc0 nt
	s_nop 0
	global_load_dwordx4 v[110:113], v[112:113], off sc0 nt
	v_addc_co_u32_e32 v129, vcc, 0, v3, vcc
	global_load_dwordx4 v[118:121], v[118:119], off sc0 nt
	s_nop 0
	global_load_dwordx4 v[122:125], v[122:123], off sc0 nt
	s_nop 0
	global_load_dwordx4 v[138:141], v[126:127], off sc0 nt
	s_nop 0
	global_load_dwordx4 v[126:129], v[128:129], off sc0 nt
	v_add_u32_e32 v144, 0, v4
	v_lshl_add_u64 v[158:159], s[2:3], 0, v[4:5]
	v_mad_u64_u32 v[160:161], s[2:3], v130, s6, v[144:145]
	s_mov_b64 s[2:3], 0x60000000
	s_nop 0
	v_lshl_add_u64 v[146:147], v[158:159], 0, s[2:3]
	ds_read_b128 v[130:133], v160
	v_lshl_add_u64 v[148:149], v[146:147], 0, v[150:151]
	s_waitcnt lgkmcnt(0)
	global_store_dwordx4 v[148:149], v[130:133], off sc1
	s_nop 1
	v_mad_u64_u32 v[162:163], s[2:3], v136, s6, v[144:145]
	ds_read_b128 v[130:133], v162
	v_lshl_add_u64 v[136:137], v[146:147], 0, v[152:153]
	s_waitcnt lgkmcnt(0)
	global_store_dwordx4 v[136:137], v[130:133], off sc1
	s_nop 1
	v_mad_u64_u32 v[164:165], s[2:3], v142, s6, v[144:145]
	ds_read_b128 v[130:133], v164
	v_lshl_add_u64 v[136:137], v[146:147], 0, v[154:155]
	s_waitcnt lgkmcnt(0)
	global_store_dwordx4 v[136:137], v[130:133], off sc1
	s_nop 1
	v_mad_u64_u32 v[166:167], s[2:3], v134, s6, v[144:145]
	ds_read_b128 v[130:133], v166
	v_lshl_add_u64 v[134:135], v[146:147], 0, v[156:157]
	s_waitcnt lgkmcnt(0)
	global_store_dwordx4 v[134:135], v[130:133], off sc1
	s_nop 1
	v_mul_f32_e32 v4, 0x43800000, v6
	v_mul_f32_e32 v6, 0x43800000, v10
	v_med3_f32 v4, v4, s5, v1
	v_med3_f32 v6, v6, s5, v1
	v_mov_b32_e32 v130, v5
	v_cvt_pk_fp8_f32 v130, v4, v6
	v_mul_f32_e32 v10, 0x43800000, v18
	v_mul_f32_e32 v4, 0x43800000, v14
	v_med3_f32 v6, v10, s5, v1
	v_med3_f32 v4, v4, s5, v1
	v_cvt_pk_fp8_f32 v130, v6, v4 op_sel:[0,0,1]
	v_mul_f32_e32 v4, 0x43800000, v22
	v_mul_f32_e32 v6, 0x43800000, v26
	v_med3_f32 v4, v4, s5, v1
	v_med3_f32 v6, v6, s5, v1
	v_mov_b32_e32 v131, v5
	v_cvt_pk_fp8_f32 v131, v4, v6
	v_mul_f32_e32 v10, 0x43800000, v42
	v_mul_f32_e32 v4, 0x43800000, v34
	v_med3_f32 v6, v10, s5, v1
	v_med3_f32 v4, v4, s5, v1
	v_cvt_pk_fp8_f32 v131, v6, v4 op_sel:[0,0,1]
	v_mul_f32_e32 v4, 0x43800000, v50
	v_mul_f32_e32 v6, 0x43800000, v54
	v_med3_f32 v4, v4, s5, v1
	v_med3_f32 v6, v6, s5, v1
	v_mov_b32_e32 v132, v5
	v_cvt_pk_fp8_f32 v132, v4, v6
	v_mul_f32_e32 v10, 0x43800000, v74
	v_mul_f32_e32 v4, 0x43800000, v70
	v_med3_f32 v6, v10, s5, v1
	v_med3_f32 v4, v4, s5, v1
	v_cvt_pk_fp8_f32 v132, v6, v4 op_sel:[0,0,1]
	v_mul_f32_e32 v4, 0x43800000, v82
	v_mul_f32_e32 v6, 0x43800000, v86
	v_med3_f32 v4, v4, s5, v1
	v_med3_f32 v6, v6, s5, v1
	v_mov_b32_e32 v133, v5
	v_cvt_pk_fp8_f32 v133, v4, v6
	v_mul_f32_e32 v10, 0x43800000, v106
	v_mul_f32_e32 v4, 0x43800000, v98
	v_med3_f32 v6, v10, s5, v1
	v_med3_f32 v4, v4, s5, v1
	v_cvt_pk_fp8_f32 v133, v6, v4 op_sel:[0,0,1]
	v_mul_f32_e32 v4, 0x43800000, v7
	v_mul_f32_e32 v6, 0x43800000, v11
	v_med3_f32 v4, v4, s5, v1
	v_med3_f32 v6, v6, s5, v1
	v_mov_b32_e32 v134, v5
	v_cvt_pk_fp8_f32 v134, v4, v6
	v_mul_f32_e32 v7, 0x43800000, v19
	v_mul_f32_e32 v4, 0x43800000, v15
	v_med3_f32 v6, v7, s5, v1
	v_med3_f32 v4, v4, s5, v1
	v_cvt_pk_fp8_f32 v134, v6, v4 op_sel:[0,0,1]
	v_mul_f32_e32 v4, 0x43800000, v23
	v_mul_f32_e32 v6, 0x43800000, v27
	v_med3_f32 v4, v4, s5, v1
	v_med3_f32 v6, v6, s5, v1
	v_mov_b32_e32 v135, v5
	v_cvt_pk_fp8_f32 v135, v4, v6
	v_mul_f32_e32 v7, 0x43800000, v43
	v_mul_f32_e32 v4, 0x43800000, v35
	v_med3_f32 v6, v7, s5, v1
	v_med3_f32 v4, v4, s5, v1
	v_cvt_pk_fp8_f32 v135, v6, v4 op_sel:[0,0,1]
	v_mul_f32_e32 v4, 0x43800000, v51
	v_mul_f32_e32 v6, 0x43800000, v55
	v_med3_f32 v4, v4, s5, v1
	v_med3_f32 v6, v6, s5, v1
	v_mov_b32_e32 v136, v5
	v_cvt_pk_fp8_f32 v136, v4, v6
	v_mul_f32_e32 v7, 0x43800000, v75
	v_mul_f32_e32 v4, 0x43800000, v71
	v_med3_f32 v6, v7, s5, v1
	v_med3_f32 v4, v4, s5, v1
	v_cvt_pk_fp8_f32 v136, v6, v4 op_sel:[0,0,1]
	v_mul_f32_e32 v4, 0x43800000, v83
	v_mul_f32_e32 v6, 0x43800000, v87
	v_med3_f32 v4, v4, s5, v1
	v_med3_f32 v6, v6, s5, v1
	v_mov_b32_e32 v137, v5
	v_cvt_pk_fp8_f32 v137, v4, v6
	v_mul_f32_e32 v7, 0x43800000, v107
	v_mul_f32_e32 v4, 0x43800000, v99
	v_med3_f32 v6, v7, s5, v1
	v_med3_f32 v4, v4, s5, v1
	v_cvt_pk_fp8_f32 v137, v6, v4 op_sel:[0,0,1]
	v_mul_f32_e32 v4, 0x43800000, v8
	v_mul_f32_e32 v6, 0x43800000, v12
	v_med3_f32 v4, v4, s5, v1
	v_med3_f32 v6, v6, s5, v1
	v_mov_b32_e32 v142, v5
	v_cvt_pk_fp8_f32 v142, v4, v6
	v_mul_f32_e32 v7, 0x43800000, v20
	v_mul_f32_e32 v4, 0x43800000, v16
	v_med3_f32 v6, v7, s5, v1
	v_med3_f32 v4, v4, s5, v1
	v_cvt_pk_fp8_f32 v142, v6, v4 op_sel:[0,0,1]
	v_mul_f32_e32 v4, 0x43800000, v24
	v_mul_f32_e32 v6, 0x43800000, v28
	v_med3_f32 v4, v4, s5, v1
	v_med3_f32 v6, v6, s5, v1
	v_mov_b32_e32 v143, v5
	v_cvt_pk_fp8_f32 v143, v4, v6
	v_mul_f32_e32 v7, 0x43800000, v44
	v_mul_f32_e32 v4, 0x43800000, v36
	v_med3_f32 v6, v7, s5, v1
	v_med3_f32 v4, v4, s5, v1
	v_cvt_pk_fp8_f32 v143, v6, v4 op_sel:[0,0,1]
	v_mul_f32_e32 v4, 0x43800000, v52
	v_mul_f32_e32 v6, 0x43800000, v56
	v_med3_f32 v4, v4, s5, v1
	v_med3_f32 v6, v6, s5, v1
	v_mov_b32_e32 v144, v5
	v_cvt_pk_fp8_f32 v144, v4, v6
	v_mul_f32_e32 v7, 0x43800000, v76
	v_mul_f32_e32 v4, 0x43800000, v72
	v_med3_f32 v6, v7, s5, v1
	v_med3_f32 v4, v4, s5, v1
	v_cvt_pk_fp8_f32 v144, v6, v4 op_sel:[0,0,1]
	v_mul_f32_e32 v4, 0x43800000, v84
	v_mul_f32_e32 v6, 0x43800000, v88
	v_med3_f32 v4, v4, s5, v1
	v_med3_f32 v6, v6, s5, v1
	v_mov_b32_e32 v145, v5
	v_cvt_pk_fp8_f32 v145, v4, v6
	v_mul_f32_e32 v7, 0x43800000, v108
	v_mul_f32_e32 v4, 0x43800000, v100
	v_med3_f32 v6, v7, s5, v1
	v_med3_f32 v4, v4, s5, v1
	v_cvt_pk_fp8_f32 v145, v6, v4 op_sel:[0,0,1]
	v_mul_f32_e32 v4, 0x43800000, v9
	v_mul_f32_e32 v6, 0x43800000, v13
	v_med3_f32 v4, v4, s5, v1
	v_med3_f32 v8, v6, s5, v1
	v_mov_b32_e32 v6, v5
	v_cvt_pk_fp8_f32 v6, v4, v8
	v_mul_f32_e32 v7, 0x43800000, v21
	v_mul_f32_e32 v4, 0x43800000, v17
	v_med3_f32 v7, v7, s5, v1
	v_med3_f32 v4, v4, s5, v1
	v_cvt_pk_fp8_f32 v6, v7, v4 op_sel:[0,0,1]
	v_mul_f32_e32 v4, 0x43800000, v25
	v_mul_f32_e32 v7, 0x43800000, v29
	v_med3_f32 v4, v4, s5, v1
	v_med3_f32 v9, v7, s5, v1
	v_mov_b32_e32 v7, v5
	v_cvt_pk_fp8_f32 v7, v4, v9
	v_mul_f32_e32 v8, 0x43800000, v45
	v_mul_f32_e32 v4, 0x43800000, v37
	v_med3_f32 v8, v8, s5, v1
	v_med3_f32 v4, v4, s5, v1
	v_cvt_pk_fp8_f32 v7, v8, v4 op_sel:[0,0,1]
	v_mul_f32_e32 v4, 0x43800000, v53
	v_mul_f32_e32 v8, 0x43800000, v57
	v_med3_f32 v4, v4, s5, v1
	v_med3_f32 v10, v8, s5, v1
	v_mov_b32_e32 v8, v5
	v_cvt_pk_fp8_f32 v8, v4, v10
	v_mul_f32_e32 v9, 0x43800000, v77
	v_mul_f32_e32 v4, 0x43800000, v73
	v_med3_f32 v9, v9, s5, v1
	v_med3_f32 v4, v4, s5, v1
	v_cvt_pk_fp8_f32 v8, v9, v4 op_sel:[0,0,1]
	v_mul_f32_e32 v4, 0x43800000, v85
	v_mul_f32_e32 v9, 0x43800000, v89
	v_med3_f32 v4, v4, s5, v1
	v_med3_f32 v11, v9, s5, v1
	v_mov_b32_e32 v9, v5
	v_cvt_pk_fp8_f32 v9, v4, v11
	v_mul_f32_e32 v10, 0x43800000, v109
	v_mul_f32_e32 v4, 0x43800000, v101
	v_med3_f32 v10, v10, s5, v1
	v_med3_f32 v4, v4, s5, v1
	v_cvt_pk_fp8_f32 v9, v10, v4 op_sel:[0,0,1]
	ds_write_b128 v168, v[130:133] offset:34816
	ds_write_b128 v168, v[134:137] offset:35088
	ds_write_b128 v168, v[142:145] offset:35360
	ds_write_b128 v168, v[6:9] offset:35632
	s_waitcnt lgkmcnt(0)
	s_barrier
	s_mov_b32 s2, 0x600000
	v_add_co_u32_e32 v6, vcc, s2, v2
	s_mov_b32 s2, 0x602000
	s_nop 0
	v_addc_co_u32_e32 v7, vcc, 0, v3, vcc
	v_add_co_u32_e32 v10, vcc, s2, v2
	s_mov_b32 s2, 0x604000
	s_nop 0
	v_addc_co_u32_e32 v11, vcc, 0, v3, vcc
	global_load_dwordx4 v[6:9], v[6:7], off sc0 nt
	s_nop 0
	global_load_dwordx4 v[14:17], v[10:11], off sc0 nt
	v_add_co_u32_e32 v10, vcc, s2, v2
	s_mov_b32 s2, 0x606000
	s_nop 0
	v_addc_co_u32_e32 v11, vcc, 0, v3, vcc
	v_add_co_u32_e32 v12, vcc, s2, v2
	s_mov_b32 s2, 0x608000
	s_nop 0
	v_addc_co_u32_e32 v13, vcc, 0, v3, vcc
	global_load_dwordx4 v[34:37], v[10:11], off sc0 nt
	global_load_dwordx4 v[22:25], v[12:13], off sc0 nt
	v_add_co_u32_e32 v10, vcc, s2, v2
	s_mov_b32 s2, 0x60a000
	s_nop 0
	v_addc_co_u32_e32 v11, vcc, 0, v3, vcc
	v_add_co_u32_e32 v12, vcc, s2, v2
	s_mov_b32 s2, 0x60c000
	s_nop 0
	v_addc_co_u32_e32 v13, vcc, 0, v3, vcc
	global_load_dwordx4 v[42:45], v[10:11], off sc0 nt
	global_load_dwordx4 v[50:53], v[12:13], off sc0 nt
	v_add_co_u32_e32 v10, vcc, s2, v2
	s_mov_b32 s2, 0x60e000
	s_nop 0
	v_addc_co_u32_e32 v11, vcc, 0, v3, vcc
	v_add_co_u32_e32 v12, vcc, s2, v2
	s_mov_b32 s2, 0x610000
	s_nop 0
	v_addc_co_u32_e32 v13, vcc, 0, v3, vcc
	global_load_dwordx4 v[70:73], v[10:11], off sc0 nt
	global_load_dwordx4 v[54:57], v[12:13], off sc0 nt
	v_add_co_u32_e32 v10, vcc, s2, v2
	s_mov_b32 s2, 0x612000
	s_nop 0
	v_addc_co_u32_e32 v11, vcc, 0, v3, vcc
	v_add_co_u32_e32 v12, vcc, s2, v2
	s_mov_b32 s2, 0x614000
	s_nop 0
	v_addc_co_u32_e32 v13, vcc, 0, v3, vcc
	global_load_dwordx4 v[74:77], v[10:11], off sc0 nt
	global_load_dwordx4 v[82:85], v[12:13], off sc0 nt
	v_add_co_u32_e32 v10, vcc, s2, v2
	s_mov_b32 s2, 0x616000
	s_nop 0
	v_addc_co_u32_e32 v11, vcc, 0, v3, vcc
	v_add_co_u32_e32 v12, vcc, s2, v2
	s_mov_b32 s2, 0x618000
	s_nop 0
	v_addc_co_u32_e32 v13, vcc, 0, v3, vcc
	global_load_dwordx4 v[106:109], v[10:11], off sc0 nt
	global_load_dwordx4 v[98:101], v[12:13], off sc0 nt
	v_add_co_u32_e32 v10, vcc, s2, v2
	s_mov_b32 s2, 0x61a000
	s_nop 0
	v_addc_co_u32_e32 v11, vcc, 0, v3, vcc
	v_add_co_u32_e32 v12, vcc, s2, v2
	s_mov_b32 s2, 0x61c000
	s_nop 0
	v_addc_co_u32_e32 v13, vcc, 0, v3, vcc
	global_load_dwordx4 v[130:133], v[10:11], off sc0 nt
	global_load_dwordx4 v[134:137], v[12:13], off sc0 nt
	v_add_co_u32_e32 v10, vcc, s2, v2
	s_mov_b32 s2, 0x61e000
	s_nop 0
	v_addc_co_u32_e32 v11, vcc, 0, v3, vcc
	v_add_co_u32_e32 v12, vcc, s2, v2
	s_nop 1
	v_addc_co_u32_e32 v13, vcc, 0, v3, vcc
	global_load_dwordx4 v[146:149], v[10:11], off sc0 nt
	global_load_dwordx4 v[142:145], v[12:13], off sc0 nt
	s_mov_b64 s[2:3], 0x60000100
	v_lshl_add_u64 v[18:19], v[158:159], 0, s[2:3]
	ds_read_b128 v[10:13], v160 offset:34816
	v_lshl_add_u64 v[20:21], v[18:19], 0, v[150:151]
	s_waitcnt lgkmcnt(0)
	global_store_dwordx4 v[20:21], v[10:13], off sc1
	s_nop 1
	ds_read_b128 v[10:13], v162 offset:34816
	v_lshl_add_u64 v[20:21], v[18:19], 0, v[152:153]
	s_waitcnt lgkmcnt(0)
	global_store_dwordx4 v[20:21], v[10:13], off sc1
	s_nop 1
	ds_read_b128 v[10:13], v164 offset:34816
	v_lshl_add_u64 v[20:21], v[18:19], 0, v[154:155]
	s_waitcnt lgkmcnt(0)
	global_store_dwordx4 v[20:21], v[10:13], off sc1
	s_nop 1
	ds_read_b128 v[10:13], v166 offset:34816
	v_lshl_add_u64 v[18:19], v[18:19], 0, v[156:157]
	s_waitcnt lgkmcnt(0)
	global_store_dwordx4 v[18:19], v[10:13], off sc1
	s_nop 1
	s_waitcnt vmcnt(31)
	v_mul_f32_e32 v4, 0x43800000, v30
	s_waitcnt vmcnt(30)
	v_mul_f32_e32 v10, 0x43800000, v38
	v_med3_f32 v4, v4, s5, v1
	v_med3_f32 v12, v10, s5, v1
	v_mov_b32_e32 v10, v5
	v_cvt_pk_fp8_f32 v10, v4, v12
	s_waitcnt vmcnt(29)
	v_mul_f32_e32 v11, 0x43800000, v58
	s_waitcnt vmcnt(28)
	v_mul_f32_e32 v4, 0x43800000, v46
	v_med3_f32 v11, v11, s5, v1
	v_med3_f32 v4, v4, s5, v1
	v_cvt_pk_fp8_f32 v10, v11, v4 op_sel:[0,0,1]
	s_waitcnt vmcnt(27)
	v_mul_f32_e32 v4, 0x43800000, v62
	s_waitcnt vmcnt(26)
	v_mul_f32_e32 v11, 0x43800000, v66
	v_med3_f32 v4, v4, s5, v1
	v_med3_f32 v13, v11, s5, v1
	v_mov_b32_e32 v11, v5
	v_cvt_pk_fp8_f32 v11, v4, v13
	s_waitcnt vmcnt(25)
	v_mul_f32_e32 v12, 0x43800000, v90
	s_waitcnt vmcnt(24)
	v_mul_f32_e32 v4, 0x43800000, v78
	v_med3_f32 v12, v12, s5, v1
	v_med3_f32 v4, v4, s5, v1
	v_cvt_pk_fp8_f32 v11, v12, v4 op_sel:[0,0,1]
	s_waitcnt vmcnt(23)
	v_mul_f32_e32 v4, 0x43800000, v94
	s_waitcnt vmcnt(22)
	v_mul_f32_e32 v12, 0x43800000, v102
	v_med3_f32 v4, v4, s5, v1
	v_med3_f32 v18, v12, s5, v1
	v_mov_b32_e32 v12, v5
	v_cvt_pk_fp8_f32 v12, v4, v18
	s_waitcnt vmcnt(21)
	v_mul_f32_e32 v13, 0x43800000, v114
	s_waitcnt vmcnt(20)
	v_mul_f32_e32 v4, 0x43800000, v110
	v_med3_f32 v13, v13, s5, v1
	v_med3_f32 v4, v4, s5, v1
	v_cvt_pk_fp8_f32 v12, v13, v4 op_sel:[0,0,1]
	s_waitcnt vmcnt(19)
	v_mul_f32_e32 v4, 0x43800000, v118
	s_waitcnt vmcnt(18)
	v_mul_f32_e32 v13, 0x43800000, v122
	v_med3_f32 v4, v4, s5, v1
	v_med3_f32 v19, v13, s5, v1
	v_mov_b32_e32 v13, v5
	v_cvt_pk_fp8_f32 v13, v4, v19
	s_waitcnt vmcnt(17)
	v_mul_f32_e32 v18, 0x43800000, v138
	s_waitcnt vmcnt(16)
	v_mul_f32_e32 v4, 0x43800000, v126
	v_med3_f32 v18, v18, s5, v1
	v_med3_f32 v4, v4, s5, v1
	v_cvt_pk_fp8_f32 v13, v18, v4 op_sel:[0,0,1]
	v_mul_f32_e32 v4, 0x43800000, v31
	v_mul_f32_e32 v18, 0x43800000, v39
	v_med3_f32 v4, v4, s5, v1
	v_med3_f32 v20, v18, s5, v1
	v_mov_b32_e32 v18, v5
	v_cvt_pk_fp8_f32 v18, v4, v20
	v_mul_f32_e32 v19, 0x43800000, v59
	v_mul_f32_e32 v4, 0x43800000, v47
	v_med3_f32 v19, v19, s5, v1
	v_med3_f32 v4, v4, s5, v1
	v_cvt_pk_fp8_f32 v18, v19, v4 op_sel:[0,0,1]
	v_mul_f32_e32 v4, 0x43800000, v63
	v_mul_f32_e32 v19, 0x43800000, v67
	v_med3_f32 v4, v4, s5, v1
	v_med3_f32 v21, v19, s5, v1
	v_mov_b32_e32 v19, v5
	v_cvt_pk_fp8_f32 v19, v4, v21
	v_mul_f32_e32 v20, 0x43800000, v91
	v_mul_f32_e32 v4, 0x43800000, v79
	v_med3_f32 v20, v20, s5, v1
	v_med3_f32 v4, v4, s5, v1
	v_cvt_pk_fp8_f32 v19, v20, v4 op_sel:[0,0,1]
	v_mul_f32_e32 v4, 0x43800000, v95
	v_mul_f32_e32 v20, 0x43800000, v103
	v_med3_f32 v4, v4, s5, v1
	v_med3_f32 v26, v20, s5, v1
	v_mov_b32_e32 v20, v5
	v_cvt_pk_fp8_f32 v20, v4, v26
	v_mul_f32_e32 v21, 0x43800000, v115
	v_mul_f32_e32 v4, 0x43800000, v111
	v_med3_f32 v21, v21, s5, v1
	v_med3_f32 v4, v4, s5, v1
	v_cvt_pk_fp8_f32 v20, v21, v4 op_sel:[0,0,1]
	v_mul_f32_e32 v4, 0x43800000, v119
	v_mul_f32_e32 v21, 0x43800000, v123
	v_med3_f32 v4, v4, s5, v1
	v_med3_f32 v27, v21, s5, v1
	v_mov_b32_e32 v21, v5
	v_cvt_pk_fp8_f32 v21, v4, v27
	v_mul_f32_e32 v26, 0x43800000, v139
	v_mul_f32_e32 v4, 0x43800000, v127
	v_med3_f32 v26, v26, s5, v1
	v_med3_f32 v4, v4, s5, v1
	v_cvt_pk_fp8_f32 v21, v26, v4 op_sel:[0,0,1]
	v_mul_f32_e32 v4, 0x43800000, v32
	v_mul_f32_e32 v26, 0x43800000, v40
	v_med3_f32 v4, v4, s5, v1
	v_med3_f32 v28, v26, s5, v1
	v_mov_b32_e32 v26, v5
	v_cvt_pk_fp8_f32 v26, v4, v28
	v_mul_f32_e32 v27, 0x43800000, v60
	v_mul_f32_e32 v4, 0x43800000, v48
	v_med3_f32 v27, v27, s5, v1
	v_med3_f32 v4, v4, s5, v1
	v_cvt_pk_fp8_f32 v26, v27, v4 op_sel:[0,0,1]
	v_mul_f32_e32 v4, 0x43800000, v64
	v_mul_f32_e32 v27, 0x43800000, v68
	v_med3_f32 v4, v4, s5, v1
	v_med3_f32 v29, v27, s5, v1
	v_mov_b32_e32 v27, v5
	v_cvt_pk_fp8_f32 v27, v4, v29
	v_mul_f32_e32 v28, 0x43800000, v92
	v_mul_f32_e32 v4, 0x43800000, v80
	v_med3_f32 v28, v28, s5, v1
	v_med3_f32 v4, v4, s5, v1
	v_cvt_pk_fp8_f32 v27, v28, v4 op_sel:[0,0,1]
	v_mul_f32_e32 v4, 0x43800000, v96
	v_mul_f32_e32 v28, 0x43800000, v104
	v_med3_f32 v4, v4, s5, v1
	v_med3_f32 v30, v28, s5, v1
	v_mov_b32_e32 v28, v5
	v_cvt_pk_fp8_f32 v28, v4, v30
	v_mul_f32_e32 v29, 0x43800000, v116
	v_mul_f32_e32 v4, 0x43800000, v112
	v_med3_f32 v29, v29, s5, v1
	v_med3_f32 v4, v4, s5, v1
	v_cvt_pk_fp8_f32 v28, v29, v4 op_sel:[0,0,1]
	v_mul_f32_e32 v4, 0x43800000, v120
	v_mul_f32_e32 v29, 0x43800000, v124
	v_med3_f32 v4, v4, s5, v1
	v_med3_f32 v31, v29, s5, v1
	v_mov_b32_e32 v29, v5
	v_cvt_pk_fp8_f32 v29, v4, v31
	v_mul_f32_e32 v30, 0x43800000, v140
	v_mul_f32_e32 v4, 0x43800000, v128
	v_med3_f32 v30, v30, s5, v1
	v_med3_f32 v4, v4, s5, v1
	v_cvt_pk_fp8_f32 v29, v30, v4 op_sel:[0,0,1]
	v_mul_f32_e32 v4, 0x43800000, v33
	v_mul_f32_e32 v30, 0x43800000, v41
	v_med3_f32 v4, v4, s5, v1
	v_med3_f32 v32, v30, s5, v1
	v_mov_b32_e32 v30, v5
	v_cvt_pk_fp8_f32 v30, v4, v32
	v_mul_f32_e32 v31, 0x43800000, v61
	v_mul_f32_e32 v4, 0x43800000, v49
	v_med3_f32 v31, v31, s5, v1
	v_med3_f32 v4, v4, s5, v1
	v_cvt_pk_fp8_f32 v30, v31, v4 op_sel:[0,0,1]
	v_mul_f32_e32 v4, 0x43800000, v65
	v_mul_f32_e32 v31, 0x43800000, v69
	v_med3_f32 v4, v4, s5, v1
	v_med3_f32 v33, v31, s5, v1
	v_mov_b32_e32 v31, v5
	v_cvt_pk_fp8_f32 v31, v4, v33
	v_mul_f32_e32 v32, 0x43800000, v93
	v_mul_f32_e32 v4, 0x43800000, v81
	v_med3_f32 v32, v32, s5, v1
	v_med3_f32 v4, v4, s5, v1
	v_cvt_pk_fp8_f32 v31, v32, v4 op_sel:[0,0,1]
	v_mul_f32_e32 v4, 0x43800000, v97
	v_mul_f32_e32 v32, 0x43800000, v105
	v_med3_f32 v4, v4, s5, v1
	v_med3_f32 v38, v32, s5, v1
	v_mov_b32_e32 v32, v5
	v_cvt_pk_fp8_f32 v32, v4, v38
	v_mul_f32_e32 v33, 0x43800000, v117
	v_mul_f32_e32 v4, 0x43800000, v113
	v_med3_f32 v33, v33, s5, v1
	v_med3_f32 v4, v4, s5, v1
	v_cvt_pk_fp8_f32 v32, v33, v4 op_sel:[0,0,1]
	v_mul_f32_e32 v4, 0x43800000, v121
	v_mul_f32_e32 v33, 0x43800000, v125
	v_med3_f32 v4, v4, s5, v1
	v_med3_f32 v39, v33, s5, v1
	v_mov_b32_e32 v33, v5
	v_cvt_pk_fp8_f32 v33, v4, v39
	v_mul_f32_e32 v38, 0x43800000, v141
	v_mul_f32_e32 v4, 0x43800000, v129
	v_med3_f32 v38, v38, s5, v1
	v_med3_f32 v4, v4, s5, v1
	v_cvt_pk_fp8_f32 v33, v38, v4 op_sel:[0,0,1]
	ds_write_b128 v168, v[10:13]
	ds_write_b128 v168, v[18:21] offset:272
	ds_write_b128 v168, v[26:29] offset:544
	ds_write_b128 v168, v[30:33] offset:816
	s_waitcnt lgkmcnt(0)
	s_barrier
	s_mov_b32 s2, 0x800000
	v_add_co_u32_e32 v10, vcc, s2, v2
	s_mov_b32 s2, 0x802000
	s_nop 0
	v_addc_co_u32_e32 v11, vcc, 0, v3, vcc
	v_add_co_u32_e32 v18, vcc, s2, v2
	s_mov_b32 s2, 0x804000
	s_nop 0
	v_addc_co_u32_e32 v19, vcc, 0, v3, vcc
	v_add_co_u32_e32 v38, vcc, s2, v2
	s_mov_b32 s2, 0x806000
	s_nop 0
	v_addc_co_u32_e32 v39, vcc, 0, v3, vcc
	v_add_co_u32_e32 v40, vcc, s2, v2
	s_mov_b32 s2, 0x808000
	s_nop 0
	v_addc_co_u32_e32 v41, vcc, 0, v3, vcc
	v_add_co_u32_e32 v58, vcc, s2, v2
	s_mov_b32 s2, 0x80a000
	s_nop 0
	v_addc_co_u32_e32 v59, vcc, 0, v3, vcc
	v_add_co_u32_e32 v60, vcc, s2, v2
	s_mov_b32 s2, 0x80c000
	s_nop 0
	v_addc_co_u32_e32 v61, vcc, 0, v3, vcc
	v_add_co_u32_e32 v66, vcc, s2, v2
	s_mov_b32 s2, 0x80e000
	s_nop 0
	v_addc_co_u32_e32 v67, vcc, 0, v3, vcc
	v_add_co_u32_e32 v68, vcc, s2, v2
	s_mov_b32 s2, 0x810000
	s_nop 0
	v_addc_co_u32_e32 v69, vcc, 0, v3, vcc
	global_load_dwordx4 v[10:13], v[10:11], off sc0 nt
	s_nop 0
	global_load_dwordx4 v[18:21], v[18:19], off sc0 nt
	s_nop 0
	global_load_dwordx4 v[30:33], v[38:39], off sc0 nt
	global_load_dwordx4 v[26:29], v[40:41], off sc0 nt
	s_nop 0
	global_load_dwordx4 v[38:41], v[58:59], off sc0 nt
	global_load_dwordx4 v[46:49], v[60:61], off sc0 nt
	global_load_dwordx4 v[62:65], v[66:67], off sc0 nt
	s_nop 0
	global_load_dwordx4 v[58:61], v[68:69], off sc0 nt
	v_add_co_u32_e32 v66, vcc, s2, v2
	s_mov_b32 s2, 0x812000
	s_nop 0
	v_addc_co_u32_e32 v67, vcc, 0, v3, vcc
	v_add_co_u32_e32 v68, vcc, s2, v2
	s_mov_b32 s2, 0x814000
	s_nop 0
	v_addc_co_u32_e32 v69, vcc, 0, v3, vcc
	global_load_dwordx4 v[78:81], v[66:67], off sc0 nt
	global_load_dwordx4 v[86:89], v[68:69], off sc0 nt
	v_add_co_u32_e32 v66, vcc, s2, v2
	s_mov_b32 s2, 0x816000
	s_nop 0
	v_addc_co_u32_e32 v67, vcc, 0, v3, vcc
	v_add_co_u32_e32 v68, vcc, s2, v2
	s_mov_b32 s2, 0x818000
	s_nop 0
	v_addc_co_u32_e32 v69, vcc, 0, v3, vcc
	global_load_dwordx4 v[102:105], v[66:67], off sc0 nt
	global_load_dwordx4 v[90:93], v[68:69], off sc0 nt
	v_add_co_u32_e32 v66, vcc, s2, v2
	s_mov_b32 s2, 0x81a000
	s_nop 0
	v_addc_co_u32_e32 v67, vcc, 0, v3, vcc
	v_add_co_u32_e32 v68, vcc, s2, v2
	s_mov_b32 s2, 0x81c000
	s_nop 0
	v_addc_co_u32_e32 v69, vcc, 0, v3, vcc
	global_load_dwordx4 v[110:113], v[66:67], off sc0 nt
	global_load_dwordx4 v[114:117], v[68:69], off sc0 nt
	v_add_co_u32_e32 v66, vcc, s2, v2
	s_mov_b32 s2, 0x81e000
	s_nop 0
	v_addc_co_u32_e32 v67, vcc, 0, v3, vcc
	v_add_co_u32_e32 v68, vcc, s2, v2
	s_nop 1
	v_addc_co_u32_e32 v69, vcc, 0, v3, vcc
	global_load_dwordx4 v[138:141], v[66:67], off sc0 nt
	global_load_dwordx4 v[122:125], v[68:69], off sc0 nt
	s_mov_b64 s[2:3], 0x60000200
	v_lshl_add_u64 v[94:95], v[158:159], 0, s[2:3]
	ds_read_b128 v[66:69], v160
	v_lshl_add_u64 v[96:97], v[94:95], 0, v[150:151]
	s_waitcnt lgkmcnt(0)
	global_store_dwordx4 v[96:97], v[66:69], off sc1
	s_nop 1
	ds_read_b128 v[66:69], v162
	v_lshl_add_u64 v[96:97], v[94:95], 0, v[152:153]
	s_waitcnt lgkmcnt(0)
	global_store_dwordx4 v[96:97], v[66:69], off sc1
	s_nop 1
	ds_read_b128 v[66:69], v164
	v_lshl_add_u64 v[96:97], v[94:95], 0, v[154:155]
	s_waitcnt lgkmcnt(0)
	global_store_dwordx4 v[96:97], v[66:69], off sc1
	s_nop 1
	ds_read_b128 v[66:69], v166
	v_lshl_add_u64 v[94:95], v[94:95], 0, v[156:157]
	s_waitcnt lgkmcnt(0)
	global_store_dwordx4 v[94:95], v[66:69], off sc1
	s_nop 1
	s_waitcnt vmcnt(31)
	v_mul_f32_e32 v4, 0x43800000, v6
	s_waitcnt vmcnt(30)
	v_mul_f32_e32 v6, 0x43800000, v14
	v_med3_f32 v4, v4, s5, v1
	v_med3_f32 v6, v6, s5, v1
	v_mov_b32_e32 v66, v5
	v_cvt_pk_fp8_f32 v66, v4, v6
	s_waitcnt vmcnt(29)
	v_mul_f32_e32 v14, 0x43800000, v34
	s_waitcnt vmcnt(28)
	v_mul_f32_e32 v4, 0x43800000, v22
	v_med3_f32 v6, v14, s5, v1
	v_med3_f32 v4, v4, s5, v1
	v_cvt_pk_fp8_f32 v66, v6, v4 op_sel:[0,0,1]
	s_waitcnt vmcnt(27)
	v_mul_f32_e32 v4, 0x43800000, v42
	s_waitcnt vmcnt(26)
	v_mul_f32_e32 v6, 0x43800000, v50
	v_med3_f32 v4, v4, s5, v1
	v_med3_f32 v6, v6, s5, v1
	v_mov_b32_e32 v67, v5
	v_cvt_pk_fp8_f32 v67, v4, v6
	s_waitcnt vmcnt(25)
	v_mul_f32_e32 v14, 0x43800000, v70
	s_waitcnt vmcnt(24)
	v_mul_f32_e32 v4, 0x43800000, v54
	v_med3_f32 v6, v14, s5, v1
	v_med3_f32 v4, v4, s5, v1
	v_cvt_pk_fp8_f32 v67, v6, v4 op_sel:[0,0,1]
	s_waitcnt vmcnt(23)
	v_mul_f32_e32 v4, 0x43800000, v74
	s_waitcnt vmcnt(22)
	v_mul_f32_e32 v6, 0x43800000, v82
	v_med3_f32 v4, v4, s5, v1
	v_med3_f32 v6, v6, s5, v1
	v_mov_b32_e32 v68, v5
	v_cvt_pk_fp8_f32 v68, v4, v6
	s_waitcnt vmcnt(21)
	v_mul_f32_e32 v14, 0x43800000, v106
	s_waitcnt vmcnt(20)
	v_mul_f32_e32 v4, 0x43800000, v98
	v_med3_f32 v6, v14, s5, v1
	v_med3_f32 v4, v4, s5, v1
	v_cvt_pk_fp8_f32 v68, v6, v4 op_sel:[0,0,1]
	s_waitcnt vmcnt(19)
	v_mul_f32_e32 v4, 0x43800000, v130
	s_waitcnt vmcnt(18)
	v_mul_f32_e32 v6, 0x43800000, v134
	v_med3_f32 v4, v4, s5, v1
	v_med3_f32 v6, v6, s5, v1
	v_mov_b32_e32 v69, v5
	v_cvt_pk_fp8_f32 v69, v4, v6
	s_waitcnt vmcnt(17)
	v_mul_f32_e32 v14, 0x43800000, v146
	s_waitcnt vmcnt(16)
	v_mul_f32_e32 v4, 0x43800000, v142
	v_med3_f32 v6, v14, s5, v1
	v_med3_f32 v4, v4, s5, v1
	v_cvt_pk_fp8_f32 v69, v6, v4 op_sel:[0,0,1]
	v_mul_f32_e32 v4, 0x43800000, v7
	v_mul_f32_e32 v6, 0x43800000, v15
	v_med3_f32 v4, v4, s5, v1
	v_med3_f32 v6, v6, s5, v1
	v_mov_b32_e32 v94, v5
	v_cvt_pk_fp8_f32 v94, v4, v6
	v_mul_f32_e32 v7, 0x43800000, v35
	v_mul_f32_e32 v4, 0x43800000, v23
	v_med3_f32 v6, v7, s5, v1
	v_med3_f32 v4, v4, s5, v1
	v_cvt_pk_fp8_f32 v94, v6, v4 op_sel:[0,0,1]
	v_mul_f32_e32 v4, 0x43800000, v43
	v_mul_f32_e32 v6, 0x43800000, v51
	v_med3_f32 v4, v4, s5, v1
	v_med3_f32 v6, v6, s5, v1
	v_mov_b32_e32 v95, v5
	v_cvt_pk_fp8_f32 v95, v4, v6
	v_mul_f32_e32 v7, 0x43800000, v71
	v_mul_f32_e32 v4, 0x43800000, v55
	v_med3_f32 v6, v7, s5, v1
	v_med3_f32 v4, v4, s5, v1
	v_cvt_pk_fp8_f32 v95, v6, v4 op_sel:[0,0,1]
	v_mul_f32_e32 v4, 0x43800000, v75
	v_mul_f32_e32 v6, 0x43800000, v83
	v_med3_f32 v4, v4, s5, v1
	v_med3_f32 v6, v6, s5, v1
	v_mov_b32_e32 v96, v5
	v_cvt_pk_fp8_f32 v96, v4, v6
	v_mul_f32_e32 v7, 0x43800000, v107
	v_mul_f32_e32 v4, 0x43800000, v99
	v_med3_f32 v6, v7, s5, v1
	v_med3_f32 v4, v4, s5, v1
	v_cvt_pk_fp8_f32 v96, v6, v4 op_sel:[0,0,1]
	v_mul_f32_e32 v4, 0x43800000, v131
	v_mul_f32_e32 v6, 0x43800000, v135
	v_med3_f32 v4, v4, s5, v1
	v_med3_f32 v6, v6, s5, v1
	v_mov_b32_e32 v97, v5
	v_cvt_pk_fp8_f32 v97, v4, v6
	v_mul_f32_e32 v7, 0x43800000, v147
	v_mul_f32_e32 v4, 0x43800000, v143
	v_med3_f32 v6, v7, s5, v1
	v_med3_f32 v4, v4, s5, v1
	v_cvt_pk_fp8_f32 v97, v6, v4 op_sel:[0,0,1]
	v_mul_f32_e32 v4, 0x43800000, v8
	v_mul_f32_e32 v6, 0x43800000, v16
	v_med3_f32 v4, v4, s5, v1
	v_med3_f32 v6, v6, s5, v1
	v_mov_b32_e32 v118, v5
	v_cvt_pk_fp8_f32 v118, v4, v6
	v_mul_f32_e32 v7, 0x43800000, v36
	v_mul_f32_e32 v4, 0x43800000, v24
	v_med3_f32 v6, v7, s5, v1
	v_med3_f32 v4, v4, s5, v1
	v_cvt_pk_fp8_f32 v118, v6, v4 op_sel:[0,0,1]
	v_mul_f32_e32 v4, 0x43800000, v44
	v_mul_f32_e32 v6, 0x43800000, v52
	v_med3_f32 v4, v4, s5, v1
	v_med3_f32 v6, v6, s5, v1
	v_mov_b32_e32 v119, v5
	v_cvt_pk_fp8_f32 v119, v4, v6
	v_mul_f32_e32 v7, 0x43800000, v72
	v_mul_f32_e32 v4, 0x43800000, v56
	v_med3_f32 v6, v7, s5, v1
	v_med3_f32 v4, v4, s5, v1
	v_cvt_pk_fp8_f32 v119, v6, v4 op_sel:[0,0,1]
	v_mul_f32_e32 v4, 0x43800000, v76
	v_mul_f32_e32 v6, 0x43800000, v84
	v_med3_f32 v4, v4, s5, v1
	v_med3_f32 v6, v6, s5, v1
	v_mov_b32_e32 v120, v5
	v_cvt_pk_fp8_f32 v120, v4, v6
	v_mul_f32_e32 v7, 0x43800000, v108
	v_mul_f32_e32 v4, 0x43800000, v100
	v_med3_f32 v6, v7, s5, v1
	v_med3_f32 v4, v4, s5, v1
	v_cvt_pk_fp8_f32 v120, v6, v4 op_sel:[0,0,1]
	v_mul_f32_e32 v4, 0x43800000, v132
	v_mul_f32_e32 v6, 0x43800000, v136
	v_med3_f32 v4, v4, s5, v1
	v_med3_f32 v6, v6, s5, v1
	v_mov_b32_e32 v121, v5
	v_cvt_pk_fp8_f32 v121, v4, v6
	v_mul_f32_e32 v7, 0x43800000, v148
	v_mul_f32_e32 v4, 0x43800000, v144
	v_med3_f32 v6, v7, s5, v1
	v_med3_f32 v4, v4, s5, v1
	v_cvt_pk_fp8_f32 v121, v6, v4 op_sel:[0,0,1]
	v_mul_f32_e32 v4, 0x43800000, v9
	v_mul_f32_e32 v6, 0x43800000, v17
	v_med3_f32 v4, v4, s5, v1
	v_med3_f32 v8, v6, s5, v1
	v_mov_b32_e32 v6, v5
	v_cvt_pk_fp8_f32 v6, v4, v8
	v_mul_f32_e32 v7, 0x43800000, v37
	v_mul_f32_e32 v4, 0x43800000, v25
	v_med3_f32 v7, v7, s5, v1
	v_med3_f32 v4, v4, s5, v1
	v_cvt_pk_fp8_f32 v6, v7, v4 op_sel:[0,0,1]
	v_mul_f32_e32 v4, 0x43800000, v45
	v_mul_f32_e32 v7, 0x43800000, v53
	v_med3_f32 v4, v4, s5, v1
	v_med3_f32 v9, v7, s5, v1
	v_mov_b32_e32 v7, v5
	v_cvt_pk_fp8_f32 v7, v4, v9
	v_mul_f32_e32 v8, 0x43800000, v73
	v_mul_f32_e32 v4, 0x43800000, v57
	v_med3_f32 v8, v8, s5, v1
	v_med3_f32 v4, v4, s5, v1
	v_cvt_pk_fp8_f32 v7, v8, v4 op_sel:[0,0,1]
	v_mul_f32_e32 v4, 0x43800000, v77
	v_mul_f32_e32 v8, 0x43800000, v85
	v_med3_f32 v4, v4, s5, v1
	v_med3_f32 v14, v8, s5, v1
	v_mov_b32_e32 v8, v5
	v_cvt_pk_fp8_f32 v8, v4, v14
	v_mul_f32_e32 v9, 0x43800000, v109
	v_mul_f32_e32 v4, 0x43800000, v101
	v_med3_f32 v9, v9, s5, v1
	v_med3_f32 v4, v4, s5, v1
	v_cvt_pk_fp8_f32 v8, v9, v4 op_sel:[0,0,1]
	v_mul_f32_e32 v4, 0x43800000, v133
	v_mul_f32_e32 v9, 0x43800000, v137
	v_med3_f32 v4, v4, s5, v1
	v_med3_f32 v15, v9, s5, v1
	v_mov_b32_e32 v9, v5
	v_cvt_pk_fp8_f32 v9, v4, v15
	v_mul_f32_e32 v14, 0x43800000, v149
	v_mul_f32_e32 v4, 0x43800000, v145
	v_med3_f32 v14, v14, s5, v1
	v_med3_f32 v4, v4, s5, v1
	v_cvt_pk_fp8_f32 v9, v14, v4 op_sel:[0,0,1]
	ds_write_b128 v168, v[66:69] offset:34816
	ds_write_b128 v168, v[94:97] offset:35088
	ds_write_b128 v168, v[118:121] offset:35360
	ds_write_b128 v168, v[6:9] offset:35632
	s_waitcnt lgkmcnt(0)
	s_barrier
	s_mov_b32 s2, 0xa00000
	v_add_co_u32_e32 v6, vcc, s2, v2
	s_mov_b32 s2, 0xa02000
	s_nop 0
	v_addc_co_u32_e32 v7, vcc, 0, v3, vcc
	v_add_co_u32_e32 v14, vcc, s2, v2
	s_mov_b32 s2, 0xa04000
	s_nop 0
	v_addc_co_u32_e32 v15, vcc, 0, v3, vcc
	v_add_co_u32_e32 v42, vcc, s2, v2
	s_mov_b32 s2, 0xa06000
	s_nop 0
	v_addc_co_u32_e32 v43, vcc, 0, v3, vcc
	v_add_co_u32_e32 v44, vcc, s2, v2
	s_mov_b32 s2, 0xa08000
	s_nop 0
	v_addc_co_u32_e32 v45, vcc, 0, v3, vcc
	v_add_co_u32_e32 v54, vcc, s2, v2
	s_mov_b32 s2, 0xa0a000
	s_nop 0
	v_addc_co_u32_e32 v55, vcc, 0, v3, vcc
	v_add_co_u32_e32 v56, vcc, s2, v2
	s_mov_b32 s2, 0xa0c000
	s_nop 0
	v_addc_co_u32_e32 v57, vcc, 0, v3, vcc
	v_add_co_u32_e32 v70, vcc, s2, v2
	s_mov_b32 s2, 0xa0e000
	s_nop 0
	v_addc_co_u32_e32 v71, vcc, 0, v3, vcc
	v_add_co_u32_e32 v72, vcc, s2, v2
	s_mov_b32 s2, 0xa10000
	s_nop 0
	v_addc_co_u32_e32 v73, vcc, 0, v3, vcc
	global_load_dwordx4 v[6:9], v[6:7], off sc0 nt
	s_nop 0
	global_load_dwordx4 v[14:17], v[14:15], off sc0 nt
	s_nop 0
	global_load_dwordx4 v[34:37], v[42:43], off sc0 nt
	global_load_dwordx4 v[22:25], v[44:45], off sc0 nt
	s_nop 0
	global_load_dwordx4 v[42:45], v[54:55], off sc0 nt
	global_load_dwordx4 v[50:53], v[56:57], off sc0 nt
	global_load_dwordx4 v[66:69], v[70:71], off sc0 nt
	s_nop 0
	global_load_dwordx4 v[54:57], v[72:73], off sc0 nt
	v_add_co_u32_e32 v70, vcc, s2, v2
	s_mov_b32 s2, 0xa12000
	s_nop 0
	v_addc_co_u32_e32 v71, vcc, 0, v3, vcc
	v_add_co_u32_e32 v74, vcc, s2, v2
	s_mov_b32 s2, 0xa14000
	s_nop 0
	v_addc_co_u32_e32 v75, vcc, 0, v3, vcc
	global_load_dwordx4 v[70:73], v[70:71], off sc0 nt
	s_nop 0
	global_load_dwordx4 v[82:85], v[74:75], off sc0 nt
	v_add_co_u32_e32 v74, vcc, s2, v2
	s_mov_b32 s2, 0xa16000
	s_nop 0
	v_addc_co_u32_e32 v75, vcc, 0, v3, vcc
	v_add_co_u32_e32 v76, vcc, s2, v2
	s_mov_b32 s2, 0xa18000
	s_nop 0
	v_addc_co_u32_e32 v77, vcc, 0, v3, vcc
	global_load_dwordx4 v[98:101], v[74:75], off sc0 nt
	global_load_dwordx4 v[94:97], v[76:77], off sc0 nt
	v_add_co_u32_e32 v74, vcc, s2, v2
	s_mov_b32 s2, 0xa1a000
	s_nop 0
	v_addc_co_u32_e32 v75, vcc, 0, v3, vcc
	v_add_co_u32_e32 v76, vcc, s2, v2
	s_mov_b32 s2, 0xa1c000
	s_nop 0
	v_addc_co_u32_e32 v77, vcc, 0, v3, vcc
	global_load_dwordx4 v[106:109], v[74:75], off sc0 nt
	global_load_dwordx4 v[118:121], v[76:77], off sc0 nt
	v_add_co_u32_e32 v74, vcc, s2, v2
	s_mov_b32 s2, 0xa1e000
	s_nop 0
	v_addc_co_u32_e32 v75, vcc, 0, v3, vcc
	v_add_co_u32_e32 v76, vcc, s2, v2
	s_nop 1
	v_addc_co_u32_e32 v77, vcc, 0, v3, vcc
	global_load_dwordx4 v[130:133], v[74:75], off sc0 nt
	global_load_dwordx4 v[126:129], v[76:77], off sc0 nt
	s_mov_b64 s[2:3], 0x60000300
	v_lshl_add_u64 v[134:135], v[158:159], 0, s[2:3]
	ds_read_b128 v[74:77], v160 offset:34816
	v_lshl_add_u64 v[136:137], v[134:135], 0, v[150:151]
	s_waitcnt lgkmcnt(0)
	global_store_dwordx4 v[136:137], v[74:77], off sc1
	s_nop 1
	ds_read_b128 v[74:77], v162 offset:34816
	v_lshl_add_u64 v[136:137], v[134:135], 0, v[152:153]
	s_waitcnt lgkmcnt(0)
	global_store_dwordx4 v[136:137], v[74:77], off sc1
	s_nop 1
	ds_read_b128 v[74:77], v164 offset:34816
	v_lshl_add_u64 v[136:137], v[134:135], 0, v[154:155]
	s_waitcnt lgkmcnt(0)
	global_store_dwordx4 v[136:137], v[74:77], off sc1
	s_nop 1
	ds_read_b128 v[74:77], v166 offset:34816
	v_lshl_add_u64 v[134:135], v[134:135], 0, v[156:157]
	s_waitcnt lgkmcnt(0)
	global_store_dwordx4 v[134:135], v[74:77], off sc1
	s_nop 1
	s_waitcnt vmcnt(31)
	v_mul_f32_e32 v4, 0x43800000, v10
	s_waitcnt vmcnt(30)
	v_mul_f32_e32 v10, 0x43800000, v18
	v_med3_f32 v4, v4, s5, v1
	v_med3_f32 v10, v10, s5, v1
	v_mov_b32_e32 v74, v5
	v_cvt_pk_fp8_f32 v74, v4, v10
	s_waitcnt vmcnt(29)
	v_mul_f32_e32 v18, 0x43800000, v30
	s_waitcnt vmcnt(28)
	v_mul_f32_e32 v4, 0x43800000, v26
	v_med3_f32 v10, v18, s5, v1
	v_med3_f32 v4, v4, s5, v1
	v_cvt_pk_fp8_f32 v74, v10, v4 op_sel:[0,0,1]
	s_waitcnt vmcnt(27)
	v_mul_f32_e32 v4, 0x43800000, v38
	s_waitcnt vmcnt(26)
	v_mul_f32_e32 v10, 0x43800000, v46
	v_med3_f32 v4, v4, s5, v1
	v_med3_f32 v10, v10, s5, v1
	v_mov_b32_e32 v75, v5
	v_cvt_pk_fp8_f32 v75, v4, v10
	s_waitcnt vmcnt(25)
	v_mul_f32_e32 v18, 0x43800000, v62
	s_waitcnt vmcnt(24)
	v_mul_f32_e32 v4, 0x43800000, v58
	v_med3_f32 v10, v18, s5, v1
	v_med3_f32 v4, v4, s5, v1
	v_cvt_pk_fp8_f32 v75, v10, v4 op_sel:[0,0,1]
	s_waitcnt vmcnt(23)
	v_mul_f32_e32 v4, 0x43800000, v78
	s_waitcnt vmcnt(22)
	v_mul_f32_e32 v10, 0x43800000, v86
	v_med3_f32 v4, v4, s5, v1
	v_med3_f32 v10, v10, s5, v1
	v_mov_b32_e32 v76, v5
	v_cvt_pk_fp8_f32 v76, v4, v10
	s_waitcnt vmcnt(21)
	v_mul_f32_e32 v18, 0x43800000, v102
	s_waitcnt vmcnt(20)
	v_mul_f32_e32 v4, 0x43800000, v90
	v_med3_f32 v10, v18, s5, v1
	v_med3_f32 v4, v4, s5, v1
	v_cvt_pk_fp8_f32 v76, v10, v4 op_sel:[0,0,1]
	s_waitcnt vmcnt(19)
	v_mul_f32_e32 v4, 0x43800000, v110
	s_waitcnt vmcnt(18)
	v_mul_f32_e32 v10, 0x43800000, v114
	v_med3_f32 v4, v4, s5, v1
	v_med3_f32 v10, v10, s5, v1
	v_mov_b32_e32 v77, v5
	v_cvt_pk_fp8_f32 v77, v4, v10
	s_waitcnt vmcnt(17)
	v_mul_f32_e32 v18, 0x43800000, v138
	s_waitcnt vmcnt(16)
	v_mul_f32_e32 v4, 0x43800000, v122
	v_med3_f32 v10, v18, s5, v1
	v_med3_f32 v4, v4, s5, v1
	v_cvt_pk_fp8_f32 v77, v10, v4 op_sel:[0,0,1]
	v_mul_f32_e32 v4, 0x43800000, v11
	v_mul_f32_e32 v10, 0x43800000, v19
	v_med3_f32 v4, v4, s5, v1
	v_med3_f32 v10, v10, s5, v1
	v_mov_b32_e32 v134, v5
	v_cvt_pk_fp8_f32 v134, v4, v10
	v_mul_f32_e32 v11, 0x43800000, v31
	v_mul_f32_e32 v4, 0x43800000, v27
	v_med3_f32 v10, v11, s5, v1
	v_med3_f32 v4, v4, s5, v1
	v_cvt_pk_fp8_f32 v134, v10, v4 op_sel:[0,0,1]
	v_mul_f32_e32 v4, 0x43800000, v39
	v_mul_f32_e32 v10, 0x43800000, v47
	v_med3_f32 v4, v4, s5, v1
	v_med3_f32 v10, v10, s5, v1
	v_mov_b32_e32 v135, v5
	v_cvt_pk_fp8_f32 v135, v4, v10
	v_mul_f32_e32 v11, 0x43800000, v63
	v_mul_f32_e32 v4, 0x43800000, v59
	v_med3_f32 v10, v11, s5, v1
	v_med3_f32 v4, v4, s5, v1
	v_cvt_pk_fp8_f32 v135, v10, v4 op_sel:[0,0,1]
	v_mul_f32_e32 v4, 0x43800000, v79
	v_mul_f32_e32 v10, 0x43800000, v87
	v_med3_f32 v4, v4, s5, v1
	v_med3_f32 v10, v10, s5, v1
	v_mov_b32_e32 v136, v5
	v_cvt_pk_fp8_f32 v136, v4, v10
	v_mul_f32_e32 v11, 0x43800000, v103
	v_mul_f32_e32 v4, 0x43800000, v91
	v_med3_f32 v10, v11, s5, v1
	v_med3_f32 v4, v4, s5, v1
	v_cvt_pk_fp8_f32 v136, v10, v4 op_sel:[0,0,1]
	v_mul_f32_e32 v4, 0x43800000, v111
	v_mul_f32_e32 v10, 0x43800000, v115
	v_med3_f32 v4, v4, s5, v1
	v_med3_f32 v10, v10, s5, v1
	v_mov_b32_e32 v137, v5
	v_cvt_pk_fp8_f32 v137, v4, v10
	v_mul_f32_e32 v11, 0x43800000, v139
	v_mul_f32_e32 v4, 0x43800000, v123
	v_med3_f32 v10, v11, s5, v1
	v_med3_f32 v4, v4, s5, v1
	v_cvt_pk_fp8_f32 v137, v10, v4 op_sel:[0,0,1]
	v_mul_f32_e32 v4, 0x43800000, v12
	v_mul_f32_e32 v10, 0x43800000, v20
	v_med3_f32 v4, v4, s5, v1
	v_med3_f32 v10, v10, s5, v1
	v_mov_b32_e32 v142, v5
	v_cvt_pk_fp8_f32 v142, v4, v10
	v_mul_f32_e32 v11, 0x43800000, v32
	v_mul_f32_e32 v4, 0x43800000, v28
	v_med3_f32 v10, v11, s5, v1
	v_med3_f32 v4, v4, s5, v1
	v_cvt_pk_fp8_f32 v142, v10, v4 op_sel:[0,0,1]
	v_mul_f32_e32 v4, 0x43800000, v40
	v_mul_f32_e32 v10, 0x43800000, v48
	v_med3_f32 v4, v4, s5, v1
	v_med3_f32 v10, v10, s5, v1
	v_mov_b32_e32 v143, v5
	v_cvt_pk_fp8_f32 v143, v4, v10
	v_mul_f32_e32 v11, 0x43800000, v64
	v_mul_f32_e32 v4, 0x43800000, v60
	v_med3_f32 v10, v11, s5, v1
	v_med3_f32 v4, v4, s5, v1
	v_cvt_pk_fp8_f32 v143, v10, v4 op_sel:[0,0,1]
	v_mul_f32_e32 v4, 0x43800000, v80
	v_mul_f32_e32 v10, 0x43800000, v88
	v_med3_f32 v4, v4, s5, v1
	v_med3_f32 v10, v10, s5, v1
	v_mov_b32_e32 v144, v5
	v_cvt_pk_fp8_f32 v144, v4, v10
	v_mul_f32_e32 v11, 0x43800000, v104
	v_mul_f32_e32 v4, 0x43800000, v92
	v_med3_f32 v10, v11, s5, v1
	v_med3_f32 v4, v4, s5, v1
	v_cvt_pk_fp8_f32 v144, v10, v4 op_sel:[0,0,1]
	v_mul_f32_e32 v4, 0x43800000, v112
	v_mul_f32_e32 v10, 0x43800000, v116
	v_med3_f32 v4, v4, s5, v1
	v_med3_f32 v10, v10, s5, v1
	v_mov_b32_e32 v145, v5
	v_cvt_pk_fp8_f32 v145, v4, v10
	v_mul_f32_e32 v11, 0x43800000, v140
	v_mul_f32_e32 v4, 0x43800000, v124
	v_med3_f32 v10, v11, s5, v1
	v_med3_f32 v4, v4, s5, v1
	v_cvt_pk_fp8_f32 v145, v10, v4 op_sel:[0,0,1]
	v_mul_f32_e32 v4, 0x43800000, v13
	v_mul_f32_e32 v10, 0x43800000, v21
	v_med3_f32 v4, v4, s5, v1
	v_med3_f32 v12, v10, s5, v1
	v_mov_b32_e32 v10, v5
	v_cvt_pk_fp8_f32 v10, v4, v12
	v_mul_f32_e32 v11, 0x43800000, v33
	v_mul_f32_e32 v4, 0x43800000, v29
	v_med3_f32 v11, v11, s5, v1
	v_med3_f32 v4, v4, s5, v1
	v_cvt_pk_fp8_f32 v10, v11, v4 op_sel:[0,0,1]
	v_mul_f32_e32 v4, 0x43800000, v41
	v_mul_f32_e32 v11, 0x43800000, v49
	v_med3_f32 v4, v4, s5, v1
	v_med3_f32 v13, v11, s5, v1
	v_mov_b32_e32 v11, v5
	v_cvt_pk_fp8_f32 v11, v4, v13
	v_mul_f32_e32 v12, 0x43800000, v65
	v_mul_f32_e32 v4, 0x43800000, v61
	v_med3_f32 v12, v12, s5, v1
	v_med3_f32 v4, v4, s5, v1
	v_cvt_pk_fp8_f32 v11, v12, v4 op_sel:[0,0,1]
	v_mul_f32_e32 v4, 0x43800000, v81
	v_mul_f32_e32 v12, 0x43800000, v89
	v_med3_f32 v4, v4, s5, v1
	v_med3_f32 v18, v12, s5, v1
	v_mov_b32_e32 v12, v5
	v_cvt_pk_fp8_f32 v12, v4, v18
	v_mul_f32_e32 v13, 0x43800000, v105
	v_mul_f32_e32 v4, 0x43800000, v93
	v_med3_f32 v13, v13, s5, v1
	v_med3_f32 v4, v4, s5, v1
	v_cvt_pk_fp8_f32 v12, v13, v4 op_sel:[0,0,1]
	v_mul_f32_e32 v4, 0x43800000, v113
	v_mul_f32_e32 v13, 0x43800000, v117
	v_med3_f32 v4, v4, s5, v1
	v_med3_f32 v19, v13, s5, v1
	v_mov_b32_e32 v13, v5
	v_cvt_pk_fp8_f32 v13, v4, v19
	v_mul_f32_e32 v18, 0x43800000, v141
	v_mul_f32_e32 v4, 0x43800000, v125
	v_med3_f32 v18, v18, s5, v1
	v_med3_f32 v4, v4, s5, v1
	v_cvt_pk_fp8_f32 v13, v18, v4 op_sel:[0,0,1]
	ds_write_b128 v168, v[74:77]
	ds_write_b128 v168, v[134:137] offset:272
	ds_write_b128 v168, v[142:145] offset:544
	ds_write_b128 v168, v[10:13] offset:816
	s_waitcnt lgkmcnt(0)
	s_barrier
	s_mov_b32 s2, 0xc00000
	v_add_co_u32_e32 v10, vcc, s2, v2
	s_mov_b32 s2, 0xc02000
	s_nop 0
	v_addc_co_u32_e32 v11, vcc, 0, v3, vcc
	v_add_co_u32_e32 v18, vcc, s2, v2
	s_mov_b32 s2, 0xc04000
	s_nop 0
	v_addc_co_u32_e32 v19, vcc, 0, v3, vcc
	v_add_co_u32_e32 v38, vcc, s2, v2
	s_mov_b32 s2, 0xc06000
	s_nop 0
	v_addc_co_u32_e32 v39, vcc, 0, v3, vcc
	v_add_co_u32_e32 v40, vcc, s2, v2
	s_mov_b32 s2, 0xc08000
	s_nop 0
	v_addc_co_u32_e32 v41, vcc, 0, v3, vcc
	v_add_co_u32_e32 v58, vcc, s2, v2
	s_mov_b32 s2, 0xc0a000
	s_nop 0
	v_addc_co_u32_e32 v59, vcc, 0, v3, vcc
	v_add_co_u32_e32 v60, vcc, s2, v2
	s_mov_b32 s2, 0xc0c000
	s_nop 0
	v_addc_co_u32_e32 v61, vcc, 0, v3, vcc
	v_add_co_u32_e32 v74, vcc, s2, v2
	s_mov_b32 s2, 0xc0e000
	s_nop 0
	v_addc_co_u32_e32 v75, vcc, 0, v3, vcc
	v_add_co_u32_e32 v76, vcc, s2, v2
	s_mov_b32 s2, 0xc10000
	s_nop 0
	v_addc_co_u32_e32 v77, vcc, 0, v3, vcc
	global_load_dwordx4 v[10:13], v[10:11], off sc0 nt
	s_nop 0
	global_load_dwordx4 v[18:21], v[18:19], off sc0 nt
	s_nop 0
	global_load_dwordx4 v[30:33], v[38:39], off sc0 nt
	global_load_dwordx4 v[26:29], v[40:41], off sc0 nt
	s_nop 0
	global_load_dwordx4 v[38:41], v[58:59], off sc0 nt
	global_load_dwordx4 v[46:49], v[60:61], off sc0 nt
	global_load_dwordx4 v[62:65], v[74:75], off sc0 nt
	s_nop 0
	global_load_dwordx4 v[58:61], v[76:77], off sc0 nt
	v_add_co_u32_e32 v74, vcc, s2, v2
	s_mov_b32 s2, 0xc12000
	s_nop 0
	v_addc_co_u32_e32 v75, vcc, 0, v3, vcc
	v_add_co_u32_e32 v78, vcc, s2, v2
	s_mov_b32 s2, 0xc14000
	s_nop 0
	v_addc_co_u32_e32 v79, vcc, 0, v3, vcc
	v_add_co_u32_e32 v86, vcc, s2, v2
	s_mov_b32 s2, 0xc16000
	s_nop 0
	v_addc_co_u32_e32 v87, vcc, 0, v3, vcc
	v_add_co_u32_e32 v88, vcc, s2, v2
	s_mov_b32 s2, 0xc18000
	s_nop 0
	v_addc_co_u32_e32 v89, vcc, 0, v3, vcc
	v_add_co_u32_e32 v102, vcc, s2, v2
	s_mov_b32 s2, 0xc1a000
	s_nop 0
	v_addc_co_u32_e32 v103, vcc, 0, v3, vcc
	v_add_co_u32_e32 v110, vcc, s2, v2
	s_mov_b32 s2, 0xc1c000
	s_nop 0
	v_addc_co_u32_e32 v111, vcc, 0, v3, vcc
	v_add_co_u32_e32 v114, vcc, s2, v2
	s_mov_b32 s2, 0xc1e000
	s_nop 0
	v_addc_co_u32_e32 v115, vcc, 0, v3, vcc
	v_add_co_u32_e32 v116, vcc, s2, v2
	global_load_dwordx4 v[74:77], v[74:75], off sc0 nt
	s_nop 0
	global_load_dwordx4 v[78:81], v[78:79], off sc0 nt
	v_addc_co_u32_e32 v117, vcc, 0, v3, vcc
	global_load_dwordx4 v[90:93], v[86:87], off sc0 nt
	s_nop 0
	global_load_dwordx4 v[86:89], v[88:89], off sc0 nt
	s_nop 0
	global_load_dwordx4 v[102:105], v[102:103], off sc0 nt
	s_nop 0
	global_load_dwordx4 v[110:113], v[110:111], off sc0 nt
	s_nop 0
	global_load_dwordx4 v[122:125], v[114:115], off sc0 nt
	s_nop 0
	global_load_dwordx4 v[114:117], v[116:117], off sc0 nt
	s_mov_b64 s[2:3], 0x60000400
	v_lshl_add_u64 v[138:139], v[158:159], 0, s[2:3]
	ds_read_b128 v[134:137], v160
	v_lshl_add_u64 v[140:141], v[138:139], 0, v[150:151]
	s_waitcnt lgkmcnt(0)
	global_store_dwordx4 v[140:141], v[134:137], off sc1
	s_nop 1
	ds_read_b128 v[134:137], v162
	v_lshl_add_u64 v[140:141], v[138:139], 0, v[152:153]
	s_waitcnt lgkmcnt(0)
	global_store_dwordx4 v[140:141], v[134:137], off sc1
	s_nop 1
	ds_read_b128 v[134:137], v164
	v_lshl_add_u64 v[140:141], v[138:139], 0, v[154:155]
	s_waitcnt lgkmcnt(0)
	global_store_dwordx4 v[140:141], v[134:137], off sc1
	s_nop 1
	ds_read_b128 v[134:137], v166
	v_lshl_add_u64 v[138:139], v[138:139], 0, v[156:157]
	s_waitcnt lgkmcnt(0)
	global_store_dwordx4 v[138:139], v[134:137], off sc1
	s_nop 1
	s_waitcnt vmcnt(31)
	v_mul_f32_e32 v4, 0x43800000, v6
	s_waitcnt vmcnt(30)
	v_mul_f32_e32 v6, 0x43800000, v14
	v_med3_f32 v4, v4, s5, v1
	v_med3_f32 v6, v6, s5, v1
	v_mov_b32_e32 v134, v5
	v_cvt_pk_fp8_f32 v134, v4, v6
	s_waitcnt vmcnt(29)
	v_mul_f32_e32 v14, 0x43800000, v34
	s_waitcnt vmcnt(28)
	v_mul_f32_e32 v4, 0x43800000, v22
	v_med3_f32 v6, v14, s5, v1
	v_med3_f32 v4, v4, s5, v1
	v_cvt_pk_fp8_f32 v134, v6, v4 op_sel:[0,0,1]
	s_waitcnt vmcnt(27)
	v_mul_f32_e32 v4, 0x43800000, v42
	s_waitcnt vmcnt(26)
	v_mul_f32_e32 v6, 0x43800000, v50
	v_med3_f32 v4, v4, s5, v1
	v_med3_f32 v6, v6, s5, v1
	v_mov_b32_e32 v135, v5
	v_cvt_pk_fp8_f32 v135, v4, v6
	s_waitcnt vmcnt(25)
	v_mul_f32_e32 v14, 0x43800000, v66
	s_waitcnt vmcnt(24)
	v_mul_f32_e32 v4, 0x43800000, v54
	v_med3_f32 v6, v14, s5, v1
	v_med3_f32 v4, v4, s5, v1
	v_cvt_pk_fp8_f32 v135, v6, v4 op_sel:[0,0,1]
	s_waitcnt vmcnt(23)
	v_mul_f32_e32 v4, 0x43800000, v70
	s_waitcnt vmcnt(22)
	v_mul_f32_e32 v6, 0x43800000, v82
	v_med3_f32 v4, v4, s5, v1
	v_med3_f32 v6, v6, s5, v1
	v_mov_b32_e32 v136, v5
	v_cvt_pk_fp8_f32 v136, v4, v6
	s_waitcnt vmcnt(21)
	v_mul_f32_e32 v14, 0x43800000, v98
	s_waitcnt vmcnt(20)
	v_mul_f32_e32 v4, 0x43800000, v94
	v_med3_f32 v6, v14, s5, v1
	v_med3_f32 v4, v4, s5, v1
	v_cvt_pk_fp8_f32 v136, v6, v4 op_sel:[0,0,1]
	s_waitcnt vmcnt(19)
	v_mul_f32_e32 v4, 0x43800000, v106
	s_waitcnt vmcnt(18)
	v_mul_f32_e32 v6, 0x43800000, v118
	v_med3_f32 v4, v4, s5, v1
	v_med3_f32 v6, v6, s5, v1
	v_mov_b32_e32 v137, v5
	v_cvt_pk_fp8_f32 v137, v4, v6
	s_waitcnt vmcnt(17)
	v_mul_f32_e32 v14, 0x43800000, v130
	s_waitcnt vmcnt(16)
	v_mul_f32_e32 v4, 0x43800000, v126
	v_med3_f32 v6, v14, s5, v1
	v_med3_f32 v4, v4, s5, v1
	v_cvt_pk_fp8_f32 v137, v6, v4 op_sel:[0,0,1]
	v_mul_f32_e32 v4, 0x43800000, v7
	v_mul_f32_e32 v6, 0x43800000, v15
	v_med3_f32 v4, v4, s5, v1
	v_med3_f32 v6, v6, s5, v1
	v_mov_b32_e32 v138, v5
	v_cvt_pk_fp8_f32 v138, v4, v6
	v_mul_f32_e32 v7, 0x43800000, v35
	v_mul_f32_e32 v4, 0x43800000, v23
	v_med3_f32 v6, v7, s5, v1
	v_med3_f32 v4, v4, s5, v1
	v_cvt_pk_fp8_f32 v138, v6, v4 op_sel:[0,0,1]
	v_mul_f32_e32 v4, 0x43800000, v43
	v_mul_f32_e32 v6, 0x43800000, v51
	v_med3_f32 v4, v4, s5, v1
	v_med3_f32 v6, v6, s5, v1
	v_mov_b32_e32 v139, v5
	v_cvt_pk_fp8_f32 v139, v4, v6
	v_mul_f32_e32 v7, 0x43800000, v67
	v_mul_f32_e32 v4, 0x43800000, v55
	v_med3_f32 v6, v7, s5, v1
	v_med3_f32 v4, v4, s5, v1
	v_cvt_pk_fp8_f32 v139, v6, v4 op_sel:[0,0,1]
	v_mul_f32_e32 v4, 0x43800000, v71
	v_mul_f32_e32 v6, 0x43800000, v83
	v_med3_f32 v4, v4, s5, v1
	v_med3_f32 v6, v6, s5, v1
	v_mov_b32_e32 v140, v5
	v_cvt_pk_fp8_f32 v140, v4, v6
	v_mul_f32_e32 v7, 0x43800000, v99
	v_mul_f32_e32 v4, 0x43800000, v95
	v_med3_f32 v6, v7, s5, v1
	v_med3_f32 v4, v4, s5, v1
	v_cvt_pk_fp8_f32 v140, v6, v4 op_sel:[0,0,1]
	v_mul_f32_e32 v4, 0x43800000, v107
	v_mul_f32_e32 v6, 0x43800000, v119
	v_med3_f32 v4, v4, s5, v1
	v_med3_f32 v6, v6, s5, v1
	v_mov_b32_e32 v141, v5
	v_cvt_pk_fp8_f32 v141, v4, v6
	v_mul_f32_e32 v7, 0x43800000, v131
	v_mul_f32_e32 v4, 0x43800000, v127
	v_med3_f32 v6, v7, s5, v1
	v_med3_f32 v4, v4, s5, v1
	v_cvt_pk_fp8_f32 v141, v6, v4 op_sel:[0,0,1]
	v_mul_f32_e32 v4, 0x43800000, v8
	v_mul_f32_e32 v6, 0x43800000, v16
	v_med3_f32 v4, v4, s5, v1
	v_med3_f32 v6, v6, s5, v1
	v_mov_b32_e32 v142, v5
	v_cvt_pk_fp8_f32 v142, v4, v6
	v_mul_f32_e32 v7, 0x43800000, v36
	v_mul_f32_e32 v4, 0x43800000, v24
	v_med3_f32 v6, v7, s5, v1
	v_med3_f32 v4, v4, s5, v1
	v_cvt_pk_fp8_f32 v142, v6, v4 op_sel:[0,0,1]
	v_mul_f32_e32 v4, 0x43800000, v44
	v_mul_f32_e32 v6, 0x43800000, v52
	v_med3_f32 v4, v4, s5, v1
	v_med3_f32 v6, v6, s5, v1
	v_mov_b32_e32 v143, v5
	v_cvt_pk_fp8_f32 v143, v4, v6
	v_mul_f32_e32 v7, 0x43800000, v68
	v_mul_f32_e32 v4, 0x43800000, v56
	v_med3_f32 v6, v7, s5, v1
	v_med3_f32 v4, v4, s5, v1
	v_cvt_pk_fp8_f32 v143, v6, v4 op_sel:[0,0,1]
	v_mul_f32_e32 v4, 0x43800000, v72
	v_mul_f32_e32 v6, 0x43800000, v84
	v_med3_f32 v4, v4, s5, v1
	v_med3_f32 v6, v6, s5, v1
	v_mov_b32_e32 v144, v5
	v_cvt_pk_fp8_f32 v144, v4, v6
	v_mul_f32_e32 v7, 0x43800000, v100
	v_mul_f32_e32 v4, 0x43800000, v96
	v_med3_f32 v6, v7, s5, v1
	v_med3_f32 v4, v4, s5, v1
	v_cvt_pk_fp8_f32 v144, v6, v4 op_sel:[0,0,1]
	v_mul_f32_e32 v4, 0x43800000, v108
	v_mul_f32_e32 v6, 0x43800000, v120
	v_med3_f32 v4, v4, s5, v1
	v_med3_f32 v6, v6, s5, v1
	v_mov_b32_e32 v145, v5
	v_cvt_pk_fp8_f32 v145, v4, v6
	v_mul_f32_e32 v7, 0x43800000, v132
	v_mul_f32_e32 v4, 0x43800000, v128
	v_med3_f32 v6, v7, s5, v1
	v_med3_f32 v4, v4, s5, v1
	v_cvt_pk_fp8_f32 v145, v6, v4 op_sel:[0,0,1]
	v_mul_f32_e32 v4, 0x43800000, v9
	v_mul_f32_e32 v6, 0x43800000, v17
	v_med3_f32 v4, v4, s5, v1
	v_med3_f32 v8, v6, s5, v1
	v_mov_b32_e32 v6, v5
	v_cvt_pk_fp8_f32 v6, v4, v8
	v_mul_f32_e32 v7, 0x43800000, v37
	v_mul_f32_e32 v4, 0x43800000, v25
	v_med3_f32 v7, v7, s5, v1
	v_med3_f32 v4, v4, s5, v1
	v_cvt_pk_fp8_f32 v6, v7, v4 op_sel:[0,0,1]
	v_mul_f32_e32 v4, 0x43800000, v45
	v_mul_f32_e32 v7, 0x43800000, v53
	v_med3_f32 v4, v4, s5, v1
	v_med3_f32 v9, v7, s5, v1
	v_mov_b32_e32 v7, v5
	v_cvt_pk_fp8_f32 v7, v4, v9
	v_mul_f32_e32 v8, 0x43800000, v69
	v_mul_f32_e32 v4, 0x43800000, v57
	v_med3_f32 v8, v8, s5, v1
	v_med3_f32 v4, v4, s5, v1
	v_cvt_pk_fp8_f32 v7, v8, v4 op_sel:[0,0,1]
	v_mul_f32_e32 v4, 0x43800000, v73
	v_mul_f32_e32 v8, 0x43800000, v85
	v_med3_f32 v4, v4, s5, v1
	v_med3_f32 v14, v8, s5, v1
	v_mov_b32_e32 v8, v5
	v_cvt_pk_fp8_f32 v8, v4, v14
	v_mul_f32_e32 v9, 0x43800000, v101
	v_mul_f32_e32 v4, 0x43800000, v97
	v_med3_f32 v9, v9, s5, v1
	v_med3_f32 v4, v4, s5, v1
	v_cvt_pk_fp8_f32 v8, v9, v4 op_sel:[0,0,1]
	v_mul_f32_e32 v4, 0x43800000, v109
	v_mul_f32_e32 v9, 0x43800000, v121
	v_med3_f32 v4, v4, s5, v1
	v_med3_f32 v15, v9, s5, v1
	v_mov_b32_e32 v9, v5
	v_cvt_pk_fp8_f32 v9, v4, v15
	v_mul_f32_e32 v14, 0x43800000, v133
	v_mul_f32_e32 v4, 0x43800000, v129
	v_med3_f32 v14, v14, s5, v1
	v_med3_f32 v4, v4, s5, v1
	v_cvt_pk_fp8_f32 v9, v14, v4 op_sel:[0,0,1]
	ds_write_b128 v168, v[134:137] offset:34816
	ds_write_b128 v168, v[138:141] offset:35088
	ds_write_b128 v168, v[142:145] offset:35360
	ds_write_b128 v168, v[6:9] offset:35632
	s_waitcnt lgkmcnt(0)
	s_barrier
	s_mov_b32 s2, 0xe00000
	v_add_co_u32_e32 v6, vcc, s2, v2
	s_mov_b32 s2, 0xe02000
	s_nop 0
	v_addc_co_u32_e32 v7, vcc, 0, v3, vcc
	v_add_co_u32_e32 v14, vcc, s2, v2
	s_mov_b32 s2, 0xe04000
	s_nop 0
	v_addc_co_u32_e32 v15, vcc, 0, v3, vcc
	v_add_co_u32_e32 v42, vcc, s2, v2
	s_mov_b32 s2, 0xe06000
	s_nop 0
	v_addc_co_u32_e32 v43, vcc, 0, v3, vcc
	v_add_co_u32_e32 v44, vcc, s2, v2
	s_mov_b32 s2, 0xe08000
	s_nop 0
	v_addc_co_u32_e32 v45, vcc, 0, v3, vcc
	v_add_co_u32_e32 v54, vcc, s2, v2
	s_mov_b32 s2, 0xe0a000
	s_nop 0
	v_addc_co_u32_e32 v55, vcc, 0, v3, vcc
	v_add_co_u32_e32 v56, vcc, s2, v2
	s_mov_b32 s2, 0xe0c000
	s_nop 0
	v_addc_co_u32_e32 v57, vcc, 0, v3, vcc
	v_add_co_u32_e32 v70, vcc, s2, v2
	s_mov_b32 s2, 0xe0e000
	s_nop 0
	v_addc_co_u32_e32 v71, vcc, 0, v3, vcc
	v_add_co_u32_e32 v72, vcc, s2, v2
	s_mov_b32 s2, 0xe10000
	s_nop 0
	v_addc_co_u32_e32 v73, vcc, 0, v3, vcc
	global_load_dwordx4 v[6:9], v[6:7], off sc0 nt
	s_nop 0
	global_load_dwordx4 v[14:17], v[14:15], off sc0 nt
	s_nop 0
	global_load_dwordx4 v[34:37], v[42:43], off sc0 nt
	global_load_dwordx4 v[22:25], v[44:45], off sc0 nt
	s_nop 0
	global_load_dwordx4 v[42:45], v[54:55], off sc0 nt
	global_load_dwordx4 v[50:53], v[56:57], off sc0 nt
	global_load_dwordx4 v[66:69], v[70:71], off sc0 nt
	s_nop 0
	global_load_dwordx4 v[54:57], v[72:73], off sc0 nt
	v_add_co_u32_e32 v70, vcc, s2, v2
	s_mov_b32 s2, 0xe12000
	s_nop 0
	v_addc_co_u32_e32 v71, vcc, 0, v3, vcc
	v_add_co_u32_e32 v82, vcc, s2, v2
	s_mov_b32 s2, 0xe14000
	s_nop 0
	v_addc_co_u32_e32 v83, vcc, 0, v3, vcc
	v_add_co_u32_e32 v94, vcc, s2, v2
	s_mov_b32 s2, 0xe16000
	s_nop 0
	v_addc_co_u32_e32 v95, vcc, 0, v3, vcc
	v_add_co_u32_e32 v96, vcc, s2, v2
	s_mov_b32 s2, 0xe18000
	s_nop 0
	v_addc_co_u32_e32 v97, vcc, 0, v3, vcc
	v_add_co_u32_e32 v106, vcc, s2, v2
	s_mov_b32 s2, 0xe1a000
	s_nop 0
	v_addc_co_u32_e32 v107, vcc, 0, v3, vcc
	v_add_co_u32_e32 v118, vcc, s2, v2
	s_mov_b32 s2, 0xe1c000
	s_nop 0
	v_addc_co_u32_e32 v119, vcc, 0, v3, vcc
	v_add_co_u32_e32 v126, vcc, s2, v2
	s_mov_b32 s2, 0xe1e000
	s_nop 0
	v_addc_co_u32_e32 v127, vcc, 0, v3, vcc
	v_add_co_u32_e32 v2, vcc, s2, v2
	global_load_dwordx4 v[70:73], v[70:71], off sc0 nt
	s_nop 0
	global_load_dwordx4 v[82:85], v[82:83], off sc0 nt
	s_nop 0
	global_load_dwordx4 v[98:101], v[94:95], off sc0 nt
	s_nop 0
	global_load_dwordx4 v[94:97], v[96:97], off sc0 nt
	s_nop 0
	global_load_dwordx4 v[106:109], v[106:107], off sc0 nt
	s_nop 0
	global_load_dwordx4 v[118:121], v[118:119], off sc0 nt
	v_addc_co_u32_e32 v3, vcc, 0, v3, vcc
	global_load_dwordx4 v[130:133], v[126:127], off sc0 nt
	s_nop 0
	global_load_dwordx4 v[126:129], v[2:3], off sc0 nt
	s_mov_b64 s[2:3], 0x60000500
	v_lshl_add_u64 v[2:3], v[158:159], 0, s[2:3]
	ds_read_b128 v[134:137], v160 offset:34816
	v_lshl_add_u64 v[138:139], v[2:3], 0, v[150:151]
	s_waitcnt lgkmcnt(0)
	global_store_dwordx4 v[138:139], v[134:137], off sc1
	s_nop 1
	ds_read_b128 v[134:137], v162 offset:34816
	v_lshl_add_u64 v[138:139], v[2:3], 0, v[152:153]
	s_waitcnt lgkmcnt(0)
	global_store_dwordx4 v[138:139], v[134:137], off sc1
	s_nop 1
	ds_read_b128 v[134:137], v164 offset:34816
	v_lshl_add_u64 v[138:139], v[2:3], 0, v[154:155]
	s_waitcnt lgkmcnt(0)
	global_store_dwordx4 v[138:139], v[134:137], off sc1
	s_nop 1
	ds_read_b128 v[134:137], v166 offset:34816
	v_lshl_add_u64 v[2:3], v[2:3], 0, v[156:157]
	s_waitcnt lgkmcnt(0)
	global_store_dwordx4 v[2:3], v[134:137], off sc1
	s_nop 1
	s_waitcnt vmcnt(31)
	v_mul_f32_e32 v2, 0x43800000, v10
	s_waitcnt vmcnt(30)
	v_mul_f32_e32 v3, 0x43800000, v18
	v_med3_f32 v2, v2, s5, v1
	v_med3_f32 v3, v3, s5, v1
	v_mov_b32_e32 v134, v5
	v_cvt_pk_fp8_f32 v134, v2, v3
	s_waitcnt vmcnt(29)
	v_mul_f32_e32 v4, 0x43800000, v30
	s_waitcnt vmcnt(28)
	v_mul_f32_e32 v2, 0x43800000, v26
	v_med3_f32 v3, v4, s5, v1
	v_med3_f32 v2, v2, s5, v1
	v_cvt_pk_fp8_f32 v134, v3, v2 op_sel:[0,0,1]
	s_waitcnt vmcnt(27)
	v_mul_f32_e32 v2, 0x43800000, v38
	s_waitcnt vmcnt(26)
	v_mul_f32_e32 v3, 0x43800000, v46
	v_med3_f32 v2, v2, s5, v1
	v_med3_f32 v3, v3, s5, v1
	v_mov_b32_e32 v135, v5
	v_cvt_pk_fp8_f32 v135, v2, v3
	s_waitcnt vmcnt(25)
	v_mul_f32_e32 v4, 0x43800000, v62
	s_waitcnt vmcnt(24)
	v_mul_f32_e32 v2, 0x43800000, v58
	v_med3_f32 v3, v4, s5, v1
	v_med3_f32 v2, v2, s5, v1
	v_cvt_pk_fp8_f32 v135, v3, v2 op_sel:[0,0,1]
	s_waitcnt vmcnt(23)
	v_mul_f32_e32 v2, 0x43800000, v74
	s_waitcnt vmcnt(22)
	v_mul_f32_e32 v3, 0x43800000, v78
	v_med3_f32 v2, v2, s5, v1
	v_med3_f32 v3, v3, s5, v1
	v_mov_b32_e32 v136, v5
	v_cvt_pk_fp8_f32 v136, v2, v3
	s_waitcnt vmcnt(21)
	v_mul_f32_e32 v4, 0x43800000, v90
	s_waitcnt vmcnt(20)
	v_mul_f32_e32 v2, 0x43800000, v86
	v_med3_f32 v3, v4, s5, v1
	v_med3_f32 v2, v2, s5, v1
	v_cvt_pk_fp8_f32 v136, v3, v2 op_sel:[0,0,1]
	s_waitcnt vmcnt(19)
	v_mul_f32_e32 v2, 0x43800000, v102
	s_waitcnt vmcnt(18)
	v_mul_f32_e32 v3, 0x43800000, v110
	v_med3_f32 v2, v2, s5, v1
	v_med3_f32 v3, v3, s5, v1
	v_mov_b32_e32 v137, v5
	v_cvt_pk_fp8_f32 v137, v2, v3
	s_waitcnt vmcnt(17)
	v_mul_f32_e32 v4, 0x43800000, v122
	s_waitcnt vmcnt(16)
	v_mul_f32_e32 v2, 0x43800000, v114
	v_med3_f32 v3, v4, s5, v1
	v_med3_f32 v2, v2, s5, v1
	v_cvt_pk_fp8_f32 v137, v3, v2 op_sel:[0,0,1]
	v_mul_f32_e32 v2, 0x43800000, v11
	v_mul_f32_e32 v3, 0x43800000, v19
	v_med3_f32 v2, v2, s5, v1
	v_med3_f32 v3, v3, s5, v1
	v_mov_b32_e32 v138, v5
	v_cvt_pk_fp8_f32 v138, v2, v3
	v_mul_f32_e32 v4, 0x43800000, v31
	v_mul_f32_e32 v2, 0x43800000, v27
	v_med3_f32 v3, v4, s5, v1
	v_med3_f32 v2, v2, s5, v1
	v_cvt_pk_fp8_f32 v138, v3, v2 op_sel:[0,0,1]
	v_mul_f32_e32 v2, 0x43800000, v39
	v_mul_f32_e32 v3, 0x43800000, v47
	v_med3_f32 v2, v2, s5, v1
	v_med3_f32 v3, v3, s5, v1
	v_mov_b32_e32 v139, v5
	v_cvt_pk_fp8_f32 v139, v2, v3
	v_mul_f32_e32 v4, 0x43800000, v63
	v_mul_f32_e32 v2, 0x43800000, v59
	v_med3_f32 v3, v4, s5, v1
	v_med3_f32 v2, v2, s5, v1
	v_cvt_pk_fp8_f32 v139, v3, v2 op_sel:[0,0,1]
	v_mul_f32_e32 v2, 0x43800000, v75
	v_mul_f32_e32 v3, 0x43800000, v79
	v_med3_f32 v2, v2, s5, v1
	v_med3_f32 v3, v3, s5, v1
	v_mov_b32_e32 v140, v5
	v_cvt_pk_fp8_f32 v140, v2, v3
	v_mul_f32_e32 v4, 0x43800000, v91
	v_mul_f32_e32 v2, 0x43800000, v87
	v_med3_f32 v3, v4, s5, v1
	v_med3_f32 v2, v2, s5, v1
	v_cvt_pk_fp8_f32 v140, v3, v2 op_sel:[0,0,1]
	v_mul_f32_e32 v2, 0x43800000, v103
	v_mul_f32_e32 v3, 0x43800000, v111
	v_med3_f32 v2, v2, s5, v1
	v_med3_f32 v3, v3, s5, v1
	v_mov_b32_e32 v141, v5
	v_cvt_pk_fp8_f32 v141, v2, v3
	v_mul_f32_e32 v4, 0x43800000, v123
	v_mul_f32_e32 v2, 0x43800000, v115
	v_med3_f32 v3, v4, s5, v1
	v_med3_f32 v2, v2, s5, v1
	v_cvt_pk_fp8_f32 v141, v3, v2 op_sel:[0,0,1]
	v_mul_f32_e32 v2, 0x43800000, v12
	v_mul_f32_e32 v3, 0x43800000, v20
	v_med3_f32 v2, v2, s5, v1
	v_med3_f32 v3, v3, s5, v1
	v_mov_b32_e32 v142, v5
	v_cvt_pk_fp8_f32 v142, v2, v3
	v_mul_f32_e32 v4, 0x43800000, v32
	v_mul_f32_e32 v2, 0x43800000, v28
	v_med3_f32 v3, v4, s5, v1
	v_med3_f32 v2, v2, s5, v1
	v_cvt_pk_fp8_f32 v142, v3, v2 op_sel:[0,0,1]
	v_mul_f32_e32 v2, 0x43800000, v40
	v_mul_f32_e32 v3, 0x43800000, v48
	v_med3_f32 v2, v2, s5, v1
	v_med3_f32 v3, v3, s5, v1
	v_mov_b32_e32 v143, v5
	v_cvt_pk_fp8_f32 v143, v2, v3
	v_mul_f32_e32 v4, 0x43800000, v64
	v_mul_f32_e32 v2, 0x43800000, v60
	v_med3_f32 v3, v4, s5, v1
	v_med3_f32 v2, v2, s5, v1
	v_cvt_pk_fp8_f32 v143, v3, v2 op_sel:[0,0,1]
	v_mul_f32_e32 v2, 0x43800000, v76
	v_mul_f32_e32 v3, 0x43800000, v80
	v_med3_f32 v2, v2, s5, v1
	v_med3_f32 v3, v3, s5, v1
	v_mov_b32_e32 v144, v5
	v_cvt_pk_fp8_f32 v144, v2, v3
	v_mul_f32_e32 v4, 0x43800000, v92
	v_mul_f32_e32 v2, 0x43800000, v88
	v_med3_f32 v3, v4, s5, v1
	v_med3_f32 v2, v2, s5, v1
	v_cvt_pk_fp8_f32 v144, v3, v2 op_sel:[0,0,1]
	v_mul_f32_e32 v2, 0x43800000, v104
	v_mul_f32_e32 v3, 0x43800000, v112
	v_med3_f32 v2, v2, s5, v1
	v_med3_f32 v3, v3, s5, v1
	v_mov_b32_e32 v145, v5
	v_cvt_pk_fp8_f32 v145, v2, v3
	v_mul_f32_e32 v4, 0x43800000, v124
	v_mul_f32_e32 v2, 0x43800000, v116
	v_med3_f32 v3, v4, s5, v1
	v_med3_f32 v2, v2, s5, v1
	v_cvt_pk_fp8_f32 v145, v3, v2 op_sel:[0,0,1]
	v_mul_f32_e32 v2, 0x43800000, v13
	v_mul_f32_e32 v3, 0x43800000, v21
	v_med3_f32 v2, v2, s5, v1
	v_med3_f32 v3, v3, s5, v1
	v_mov_b32_e32 v10, v5
	v_cvt_pk_fp8_f32 v10, v2, v3
	v_mul_f32_e32 v4, 0x43800000, v33
	v_mul_f32_e32 v2, 0x43800000, v29
	v_med3_f32 v3, v4, s5, v1
	v_med3_f32 v2, v2, s5, v1
	v_cvt_pk_fp8_f32 v10, v3, v2 op_sel:[0,0,1]
	v_mul_f32_e32 v2, 0x43800000, v41
	v_mul_f32_e32 v3, 0x43800000, v49
	v_med3_f32 v2, v2, s5, v1
	v_med3_f32 v3, v3, s5, v1
	v_mov_b32_e32 v11, v5
	v_cvt_pk_fp8_f32 v11, v2, v3
	v_mul_f32_e32 v4, 0x43800000, v65
	v_mul_f32_e32 v2, 0x43800000, v61
	v_med3_f32 v3, v4, s5, v1
	v_med3_f32 v2, v2, s5, v1
	v_cvt_pk_fp8_f32 v11, v3, v2 op_sel:[0,0,1]
	v_mul_f32_e32 v2, 0x43800000, v77
	v_mul_f32_e32 v3, 0x43800000, v81
	v_med3_f32 v2, v2, s5, v1
	v_med3_f32 v3, v3, s5, v1
	v_mov_b32_e32 v12, v5
	v_cvt_pk_fp8_f32 v12, v2, v3
	v_mul_f32_e32 v4, 0x43800000, v93
	v_mul_f32_e32 v2, 0x43800000, v89
	v_med3_f32 v3, v4, s5, v1
	v_med3_f32 v2, v2, s5, v1
	v_cvt_pk_fp8_f32 v12, v3, v2 op_sel:[0,0,1]
	v_mul_f32_e32 v2, 0x43800000, v105
	v_mul_f32_e32 v3, 0x43800000, v113
	v_med3_f32 v2, v2, s5, v1
	v_med3_f32 v3, v3, s5, v1
	v_mov_b32_e32 v13, v5
	v_cvt_pk_fp8_f32 v13, v2, v3
	v_mul_f32_e32 v4, 0x43800000, v125
	v_mul_f32_e32 v2, 0x43800000, v117
	v_med3_f32 v3, v4, s5, v1
	v_med3_f32 v2, v2, s5, v1
	v_cvt_pk_fp8_f32 v13, v3, v2 op_sel:[0,0,1]
	ds_write_b128 v168, v[134:137]
	ds_write_b128 v168, v[138:141] offset:272
	ds_write_b128 v168, v[142:145] offset:544
	ds_write_b128 v168, v[10:13] offset:816
	s_waitcnt lgkmcnt(0)
	s_barrier
	s_mov_b64 s[2:3], 0x60000600
	v_lshl_add_u64 v[2:3], v[158:159], 0, s[2:3]
	ds_read_b128 v[10:13], v160
	v_lshl_add_u64 v[18:19], v[2:3], 0, v[150:151]
	s_waitcnt lgkmcnt(0)
	global_store_dwordx4 v[18:19], v[10:13], off sc1
	s_nop 1
	ds_read_b128 v[10:13], v162
	v_lshl_add_u64 v[18:19], v[2:3], 0, v[152:153]
	s_waitcnt lgkmcnt(0)
	global_store_dwordx4 v[18:19], v[10:13], off sc1
	s_nop 1
	ds_read_b128 v[10:13], v164
	v_lshl_add_u64 v[18:19], v[2:3], 0, v[154:155]
	s_waitcnt lgkmcnt(0)
	global_store_dwordx4 v[18:19], v[10:13], off sc1
	s_nop 1
	ds_read_b128 v[10:13], v166
	v_lshl_add_u64 v[2:3], v[2:3], 0, v[156:157]
	s_waitcnt lgkmcnt(0)
	global_store_dwordx4 v[2:3], v[10:13], off sc1
	s_nop 1
	s_waitcnt vmcnt(15)
	v_mul_f32_e32 v2, 0x43800000, v6
	s_waitcnt vmcnt(14)
	v_mul_f32_e32 v3, 0x43800000, v14
	v_med3_f32 v2, v2, s5, v1
	v_med3_f32 v3, v3, s5, v1
	v_mov_b32_e32 v10, v5
	v_cvt_pk_fp8_f32 v10, v2, v3
	s_waitcnt vmcnt(13)
	v_mul_f32_e32 v4, 0x43800000, v34
	s_waitcnt vmcnt(12)
	v_mul_f32_e32 v2, 0x43800000, v22
	v_med3_f32 v3, v4, s5, v1
	v_med3_f32 v2, v2, s5, v1
	v_cvt_pk_fp8_f32 v10, v3, v2 op_sel:[0,0,1]
	s_waitcnt vmcnt(11)
	v_mul_f32_e32 v2, 0x43800000, v42
	s_waitcnt vmcnt(10)
	v_mul_f32_e32 v3, 0x43800000, v50
	v_med3_f32 v2, v2, s5, v1
	v_med3_f32 v3, v3, s5, v1
	v_mov_b32_e32 v11, v5
	v_cvt_pk_fp8_f32 v11, v2, v3
	s_waitcnt vmcnt(9)
	v_mul_f32_e32 v4, 0x43800000, v66
	s_waitcnt vmcnt(8)
	v_mul_f32_e32 v2, 0x43800000, v54
	v_med3_f32 v3, v4, s5, v1
	v_med3_f32 v2, v2, s5, v1
	v_cvt_pk_fp8_f32 v11, v3, v2 op_sel:[0,0,1]
	s_waitcnt vmcnt(7)
	v_mul_f32_e32 v2, 0x43800000, v70
	s_waitcnt vmcnt(6)
	v_mul_f32_e32 v3, 0x43800000, v82
	v_med3_f32 v2, v2, s5, v1
	v_med3_f32 v3, v3, s5, v1
	v_mov_b32_e32 v12, v5
	v_cvt_pk_fp8_f32 v12, v2, v3
	s_waitcnt vmcnt(5)
	v_mul_f32_e32 v4, 0x43800000, v98
	s_waitcnt vmcnt(4)
	v_mul_f32_e32 v2, 0x43800000, v94
	v_med3_f32 v3, v4, s5, v1
	v_med3_f32 v2, v2, s5, v1
	v_cvt_pk_fp8_f32 v12, v3, v2 op_sel:[0,0,1]
	s_waitcnt vmcnt(3)
	v_mul_f32_e32 v2, 0x43800000, v106
	s_waitcnt vmcnt(2)
	v_mul_f32_e32 v3, 0x43800000, v118
	v_med3_f32 v2, v2, s5, v1
	v_med3_f32 v3, v3, s5, v1
	v_mov_b32_e32 v13, v5
	v_cvt_pk_fp8_f32 v13, v2, v3
	s_waitcnt vmcnt(1)
	v_mul_f32_e32 v4, 0x43800000, v130
	s_waitcnt vmcnt(0)
	v_mul_f32_e32 v2, 0x43800000, v126
	v_med3_f32 v3, v4, s5, v1
	v_med3_f32 v2, v2, s5, v1
	v_cvt_pk_fp8_f32 v13, v3, v2 op_sel:[0,0,1]
	v_mul_f32_e32 v2, 0x43800000, v7
	v_mul_f32_e32 v3, 0x43800000, v15
	v_med3_f32 v2, v2, s5, v1
	v_med3_f32 v3, v3, s5, v1
	v_mov_b32_e32 v18, v5
	v_cvt_pk_fp8_f32 v18, v2, v3
	v_mul_f32_e32 v4, 0x43800000, v35
	v_mul_f32_e32 v2, 0x43800000, v23
	v_med3_f32 v3, v4, s5, v1
	v_med3_f32 v2, v2, s5, v1
	v_cvt_pk_fp8_f32 v18, v3, v2 op_sel:[0,0,1]
	v_mul_f32_e32 v2, 0x43800000, v43
	v_mul_f32_e32 v3, 0x43800000, v51
	v_med3_f32 v2, v2, s5, v1
	v_med3_f32 v3, v3, s5, v1
	v_mov_b32_e32 v19, v5
	v_cvt_pk_fp8_f32 v19, v2, v3
	v_mul_f32_e32 v4, 0x43800000, v67
	v_mul_f32_e32 v2, 0x43800000, v55
	v_med3_f32 v3, v4, s5, v1
	v_med3_f32 v2, v2, s5, v1
	v_cvt_pk_fp8_f32 v19, v3, v2 op_sel:[0,0,1]
	v_mul_f32_e32 v2, 0x43800000, v71
	v_mul_f32_e32 v3, 0x43800000, v83
	v_med3_f32 v2, v2, s5, v1
	v_med3_f32 v3, v3, s5, v1
	v_mov_b32_e32 v20, v5
	v_cvt_pk_fp8_f32 v20, v2, v3
	v_mul_f32_e32 v4, 0x43800000, v99
	v_mul_f32_e32 v2, 0x43800000, v95
	v_med3_f32 v3, v4, s5, v1
	v_med3_f32 v2, v2, s5, v1
	v_cvt_pk_fp8_f32 v20, v3, v2 op_sel:[0,0,1]
	v_mul_f32_e32 v2, 0x43800000, v107
	v_mul_f32_e32 v3, 0x43800000, v119
	v_med3_f32 v2, v2, s5, v1
	v_med3_f32 v3, v3, s5, v1
	v_mov_b32_e32 v21, v5
	v_cvt_pk_fp8_f32 v21, v2, v3
	v_mul_f32_e32 v4, 0x43800000, v131
	v_mul_f32_e32 v2, 0x43800000, v127
	v_med3_f32 v3, v4, s5, v1
	v_med3_f32 v2, v2, s5, v1
	v_cvt_pk_fp8_f32 v21, v3, v2 op_sel:[0,0,1]
	v_mul_f32_e32 v2, 0x43800000, v8
	v_mul_f32_e32 v3, 0x43800000, v16
	v_med3_f32 v2, v2, s5, v1
	v_med3_f32 v3, v3, s5, v1
	v_mov_b32_e32 v26, v5
	v_cvt_pk_fp8_f32 v26, v2, v3
	v_mul_f32_e32 v4, 0x43800000, v36
	v_mul_f32_e32 v2, 0x43800000, v24
	v_med3_f32 v3, v4, s5, v1
	v_med3_f32 v2, v2, s5, v1
	v_cvt_pk_fp8_f32 v26, v3, v2 op_sel:[0,0,1]
	v_mul_f32_e32 v2, 0x43800000, v44
	v_mul_f32_e32 v3, 0x43800000, v52
	v_med3_f32 v2, v2, s5, v1
	v_med3_f32 v3, v3, s5, v1
	v_mov_b32_e32 v27, v5
	v_cvt_pk_fp8_f32 v27, v2, v3
	v_mul_f32_e32 v4, 0x43800000, v68
	v_mul_f32_e32 v2, 0x43800000, v56
	v_med3_f32 v3, v4, s5, v1
	v_med3_f32 v2, v2, s5, v1
	v_cvt_pk_fp8_f32 v27, v3, v2 op_sel:[0,0,1]
	v_mul_f32_e32 v2, 0x43800000, v72
	v_mul_f32_e32 v3, 0x43800000, v84
	v_med3_f32 v2, v2, s5, v1
	v_med3_f32 v3, v3, s5, v1
	v_mov_b32_e32 v28, v5
	v_cvt_pk_fp8_f32 v28, v2, v3
	v_mul_f32_e32 v4, 0x43800000, v100
	v_mul_f32_e32 v2, 0x43800000, v96
	v_med3_f32 v3, v4, s5, v1
	v_med3_f32 v2, v2, s5, v1
	v_cvt_pk_fp8_f32 v28, v3, v2 op_sel:[0,0,1]
	v_mul_f32_e32 v2, 0x43800000, v108
	v_mul_f32_e32 v3, 0x43800000, v120
	v_med3_f32 v2, v2, s5, v1
	v_med3_f32 v3, v3, s5, v1
	v_mov_b32_e32 v29, v5
	v_cvt_pk_fp8_f32 v29, v2, v3
	v_mul_f32_e32 v4, 0x43800000, v132
	v_mul_f32_e32 v2, 0x43800000, v128
	v_med3_f32 v3, v4, s5, v1
	v_med3_f32 v2, v2, s5, v1
	v_cvt_pk_fp8_f32 v29, v3, v2 op_sel:[0,0,1]
	v_mul_f32_e32 v2, 0x43800000, v9
	v_mul_f32_e32 v3, 0x43800000, v17
	v_med3_f32 v6, v2, s5, v1
	v_med3_f32 v3, v3, s5, v1
	v_mov_b32_e32 v2, v5
	v_cvt_pk_fp8_f32 v2, v6, v3
	v_mul_f32_e32 v4, 0x43800000, v37
	v_mul_f32_e32 v3, 0x43800000, v25
	v_med3_f32 v4, v4, s5, v1
	v_med3_f32 v3, v3, s5, v1
	v_cvt_pk_fp8_f32 v2, v4, v3 op_sel:[0,0,1]
	v_mul_f32_e32 v3, 0x43800000, v45
	v_mul_f32_e32 v4, 0x43800000, v53
	v_med3_f32 v7, v3, s5, v1
	v_med3_f32 v4, v4, s5, v1
	v_mov_b32_e32 v3, v5
	v_cvt_pk_fp8_f32 v3, v7, v4
	v_mul_f32_e32 v6, 0x43800000, v69
	v_mul_f32_e32 v4, 0x43800000, v57
	v_med3_f32 v6, v6, s5, v1
	v_med3_f32 v4, v4, s5, v1
	v_cvt_pk_fp8_f32 v3, v6, v4 op_sel:[0,0,1]
	v_mul_f32_e32 v4, 0x43800000, v73
	v_mul_f32_e32 v6, 0x43800000, v85
	v_med3_f32 v8, v4, s5, v1
	v_med3_f32 v6, v6, s5, v1
	v_mov_b32_e32 v4, v5
	v_cvt_pk_fp8_f32 v4, v8, v6
	v_mul_f32_e32 v7, 0x43800000, v101
	v_mul_f32_e32 v6, 0x43800000, v97
	v_med3_f32 v7, v7, s5, v1
	v_med3_f32 v6, v6, s5, v1
	v_cvt_pk_fp8_f32 v4, v7, v6 op_sel:[0,0,1]
	v_mul_f32_e32 v6, 0x43800000, v109
	v_mul_f32_e32 v7, 0x43800000, v121
	v_med3_f32 v6, v6, s5, v1
	v_med3_f32 v7, v7, s5, v1
	v_cvt_pk_fp8_f32 v5, v6, v7
	v_mul_f32_e32 v8, 0x43800000, v133
	v_mul_f32_e32 v6, 0x43800000, v129
	v_med3_f32 v7, v8, s5, v1
	v_med3_f32 v1, v6, s5, v1
	v_cvt_pk_fp8_f32 v5, v7, v1 op_sel:[0,0,1]
	ds_write_b128 v168, v[10:13] offset:34816
	ds_write_b128 v168, v[18:21] offset:35088
	ds_write_b128 v168, v[26:29] offset:35360
	ds_write_b128 v168, v[2:5] offset:35632
	s_waitcnt lgkmcnt(0)
	s_barrier
	s_mov_b64 s[2:3], 0x60000700
	v_lshl_add_u64 v[6:7], v[158:159], 0, s[2:3]
	ds_read_b128 v[2:5], v160 offset:34816
	v_lshl_add_u64 v[8:9], v[6:7], 0, v[150:151]
	s_waitcnt lgkmcnt(0)
	global_store_dwordx4 v[8:9], v[2:5], off sc1
	s_nop 1
	ds_read_b128 v[2:5], v162 offset:34816
	v_lshl_add_u64 v[8:9], v[6:7], 0, v[152:153]
	s_waitcnt lgkmcnt(0)
	global_store_dwordx4 v[8:9], v[2:5], off sc1
	s_nop 1
	ds_read_b128 v[2:5], v164 offset:34816
	v_lshl_add_u64 v[8:9], v[6:7], 0, v[154:155]
	s_waitcnt lgkmcnt(0)
	global_store_dwordx4 v[8:9], v[2:5], off sc1
	s_nop 1
	ds_read_b128 v[2:5], v166 offset:34816
	v_lshl_add_u64 v[6:7], v[6:7], 0, v[156:157]
	s_waitcnt lgkmcnt(0)
	global_store_dwordx4 v[6:7], v[2:5], off sc1
	s_nop 1
	s_barrier
	s_waitcnt vmcnt(0)
	v_cmp_gt_u32_e32 vcc, 32, v0
	s_barrier
	s_and_saveexec_b64 s[2:3], vcc
	s_cbranch_execz .LBB0_1245
	v_lshlrev_b32_e32 v1, 4, v0
	v_lshl_or_b32 v2, s4, 9, v1
	v_ashrrev_i32_e32 v3, 31, v2
	v_lshl_add_u64 v[2:3], v[2:3], 2, s[14:15]
	v_mov_b32_e32 v1, 1
	global_atomic_add v[2:3], v1, off

.LBB0_1381:
	s_ashr_i32 s3, s0, 11
	s_mul_hi_i32 s5, s3, 0xc000
	s_mul_i32 s3, s3, 0xc000
	s_add_u32 s3, s78, s3
	s_addc_u32 s20, s79, s5
	s_ashr_i32 s5, s4, 31
	s_lshl_b64 s[16:17], s[4:5], 2
	s_add_u32 s18, s11, s16
	s_addc_u32 s19, s12, s17
	global_load_dwordx4 v[16:19], v41, s[18:19]
	s_add_u32 s16, s13, s16
	s_addc_u32 s17, s14, s17
	global_load_dword v27, v41, s[16:17]
	s_add_i32 s18, s4, 1
	s_ashr_i32 s19, s18, 31
	s_lshl_b64 s[16:17], s[18:19], 2
	s_add_u32 s16, s13, s16
	s_addc_u32 s17, s14, s17
	global_load_dwordx3 v[24:26], v41, s[16:17]
	global_load_dwordx4 v[52:55], v[46:47], off sc0 nt
	global_load_dwordx4 v[92:95], v[46:47], off offset:1024 sc0 nt
	global_load_dwordx4 v[36:39], v[46:47], off offset:2048 sc0 nt
	global_load_dwordx4 v[32:35], v[46:47], off offset:3072 sc0 nt
	s_add_u32 s16, s3, 0x40a000
	s_addc_u32 s17, s20, 0
	global_load_dwordx4 v[4:7], v40, s[16:17] offset:16
	global_load_dwordx4 v[12:15], v40, s[16:17]
	global_load_dwordx4 v[0:3], v120, s[16:17] offset:16
	global_load_dwordx4 v[8:11], v120, s[16:17]
	s_waitcnt vmcnt(10)
	v_lshlrev_b32_e32 v16, 2, v16
	v_lshlrev_b32_e32 v17, 2, v17
	v_lshlrev_b32_e32 v18, 2, v18
	v_lshlrev_b32_e32 v19, 2, v19
	v_add_u32_e32 v16, s1, v16
	v_add_u32_e32 v17, s1, v17
	v_add_u32_e32 v18, s1, v18
	v_add_u32_e32 v19, s1, v19
	ds_read_b32 v28, v16
	ds_read_b32 v29, v17
	ds_read_b32 v30, v18
	ds_read_b32 v31, v19
	global_load_dwordx4 v[16:19], v121, s[16:17] offset:16
	global_load_dwordx4 v[20:23], v121, s[16:17]
	s_waitcnt vmcnt(11) lgkmcnt(3)
	v_add_u32_e32 v28, v27, v28
	s_waitcnt vmcnt(10) lgkmcnt(2)
	v_add_u32_e32 v24, v24, v29
	s_waitcnt lgkmcnt(1)
	v_add_u32_e32 v30, v25, v30
	s_waitcnt lgkmcnt(0)
	v_add_u32_e32 v26, v26, v31
	v_ashrrev_i32_e32 v29, 31, v28
	v_ashrrev_i32_e32 v25, 31, v24
	v_ashrrev_i32_e32 v31, 31, v30
	v_ashrrev_i32_e32 v27, 31, v26
	v_lshlrev_b64 v[28:29], 11, v[28:29]
	v_lshlrev_b64 v[24:25], 11, v[24:25]
	v_lshlrev_b64 v[30:31], 11, v[30:31]
	v_lshlrev_b64 v[26:27], 11, v[26:27]
	v_lshl_add_u64 v[28:29], v[42:43], 0, v[28:29]
	v_lshl_add_u64 v[24:25], v[42:43], 0, v[24:25]
	v_lshl_add_u64 v[30:31], v[42:43], 0, v[30:31]
	v_lshl_add_u64 v[48:49], v[42:43], 0, v[26:27]
	global_load_dwordx2 v[50:51], v[28:29], off nt
	global_load_dwordx2 v[88:89], v[28:29], off offset:512 nt
	global_load_dwordx2 v[124:125], v[28:29], off offset:1024 nt
	global_load_dwordx2 v[118:119], v[28:29], off offset:1536 nt
	global_load_dwordx2 v[56:57], v[24:25], off nt
	global_load_dwordx2 v[90:91], v[24:25], off offset:512 nt
	global_load_dwordx2 v[126:127], v[24:25], off offset:1024 nt
	global_load_dwordx2 v[108:109], v[24:25], off offset:1536 nt
	global_load_dwordx2 v[58:59], v[30:31], off nt
	global_load_dwordx2 v[96:97], v[30:31], off offset:512 nt
	global_load_dwordx2 v[128:129], v[30:31], off offset:1024 nt
	global_load_dwordx2 v[104:105], v[30:31], off offset:1536 nt
	global_load_dwordx2 v[62:63], v[48:49], off nt
	global_load_dwordx2 v[102:103], v[48:49], off offset:512 nt
	global_load_dwordx2 v[130:131], v[48:49], off offset:1024 nt
	global_load_dwordx2 v[106:107], v[48:49], off offset:1536 nt
	global_load_dwordx4 v[24:27], v122, s[16:17] offset:16
	global_load_dwordx4 v[28:31], v122, s[16:17]
	s_waitcnt vmcnt(17)
	v_cvt_pk_f32_fp8_e32 v[80:81], v50
	v_cvt_pk_f32_fp8_sdwa v[82:83], v50 src0_sel:WORD_1
	v_cvt_pk_f32_fp8_e32 v[84:85], v51
	v_cvt_pk_f32_fp8_sdwa v[86:87], v51 src0_sel:WORD_1
	s_waitcnt vmcnt(13)
	v_cvt_pk_f32_fp8_e32 v[72:73], v56
	v_cvt_pk_f32_fp8_sdwa v[76:77], v56 src0_sel:WORD_1
	v_cvt_pk_f32_fp8_e32 v[132:133], v88
	v_cvt_pk_f32_fp8_sdwa v[134:135], v88 src0_sel:WORD_1
	v_cvt_pk_f32_fp8_e32 v[136:137], v89
	v_cvt_pk_f32_fp8_sdwa v[138:139], v89 src0_sel:WORD_1
	v_cvt_pk_f32_fp8_e32 v[148:149], v124
	v_cvt_pk_f32_fp8_sdwa v[150:151], v124 src0_sel:WORD_1
	v_cvt_pk_f32_fp8_e32 v[152:153], v125
	v_cvt_pk_f32_fp8_sdwa v[124:125], v125 src0_sel:WORD_1
	v_cvt_pk_f32_fp8_e32 v[176:177], v118
	v_cvt_pk_f32_fp8_sdwa v[178:179], v118 src0_sel:WORD_1
	v_cvt_pk_f32_fp8_e32 v[180:181], v119
	v_cvt_pk_f32_fp8_sdwa v[118:119], v119 src0_sel:WORD_1
	v_cvt_pk_f32_fp8_e32 v[74:75], v57
	v_cvt_pk_f32_fp8_sdwa v[78:79], v57 src0_sel:WORD_1
	s_waitcnt vmcnt(9)
	v_cvt_pk_f32_fp8_e32 v[64:65], v58
	v_cvt_pk_f32_fp8_sdwa v[66:67], v58 src0_sel:WORD_1
	v_cvt_pk_f32_fp8_e32 v[140:141], v90
	v_cvt_pk_f32_fp8_sdwa v[142:143], v90 src0_sel:WORD_1
	v_cvt_pk_f32_fp8_e32 v[144:145], v91
	v_cvt_pk_f32_fp8_sdwa v[146:147], v91 src0_sel:WORD_1
	v_cvt_pk_f32_fp8_e32 v[154:155], v126
	v_cvt_pk_f32_fp8_sdwa v[156:157], v126 src0_sel:WORD_1
	v_cvt_pk_f32_fp8_e32 v[158:159], v127
	v_cvt_pk_f32_fp8_sdwa v[126:127], v127 src0_sel:WORD_1
	v_cvt_pk_f32_fp8_e32 v[182:183], v108
	v_cvt_pk_f32_fp8_sdwa v[184:185], v108 src0_sel:WORD_1
	v_cvt_pk_f32_fp8_e32 v[186:187], v109
	v_cvt_pk_f32_fp8_sdwa v[108:109], v109 src0_sel:WORD_1
	v_cvt_pk_f32_fp8_e32 v[68:69], v59
	v_cvt_pk_f32_fp8_sdwa v[70:71], v59 src0_sel:WORD_1
	s_waitcnt vmcnt(5)
	v_cvt_pk_f32_fp8_e32 v[56:57], v62
	v_cvt_pk_f32_fp8_sdwa v[60:61], v62 src0_sel:WORD_1
	v_cvt_pk_f32_fp8_e32 v[110:111], v96
	v_cvt_pk_f32_fp8_sdwa v[112:113], v96 src0_sel:WORD_1
	v_cvt_pk_f32_fp8_e32 v[114:115], v97
	v_cvt_pk_f32_fp8_sdwa v[116:117], v97 src0_sel:WORD_1
	v_cvt_pk_f32_fp8_e32 v[160:161], v128
	v_cvt_pk_f32_fp8_sdwa v[162:163], v128 src0_sel:WORD_1
	v_cvt_pk_f32_fp8_e32 v[164:165], v129
	v_cvt_pk_f32_fp8_sdwa v[128:129], v129 src0_sel:WORD_1
	v_cvt_pk_f32_fp8_e32 v[188:189], v104
	v_cvt_pk_f32_fp8_sdwa v[190:191], v104 src0_sel:WORD_1
	v_cvt_pk_f32_fp8_e32 v[192:193], v105
	v_cvt_pk_f32_fp8_sdwa v[104:105], v105 src0_sel:WORD_1
	v_cvt_pk_f32_fp8_e32 v[58:59], v63
	v_cvt_pk_f32_fp8_sdwa v[62:63], v63 src0_sel:WORD_1
	s_waitcnt vmcnt(4)
	v_cvt_pk_f32_fp8_e32 v[96:97], v102
	v_cvt_pk_f32_fp8_sdwa v[100:101], v102 src0_sel:WORD_1
	v_cvt_pk_f32_fp8_e32 v[98:99], v103
	v_cvt_pk_f32_fp8_sdwa v[102:103], v103 src0_sel:WORD_1
	s_waitcnt vmcnt(3)
	v_cvt_pk_f32_fp8_e32 v[166:167], v130
	v_cvt_pk_f32_fp8_sdwa v[168:169], v130 src0_sel:WORD_1
	v_cvt_pk_f32_fp8_e32 v[170:171], v131
	v_cvt_pk_f32_fp8_sdwa v[130:131], v131 src0_sel:WORD_1
	s_waitcnt vmcnt(2)
	v_cvt_pk_f32_fp8_e32 v[194:195], v106
	v_cvt_pk_f32_fp8_sdwa v[196:197], v106 src0_sel:WORD_1
	v_cvt_pk_f32_fp8_e32 v[198:199], v107
	v_cvt_pk_f32_fp8_sdwa v[106:107], v107 src0_sel:WORD_1
	v_pk_add_f32 v[80:81], v[80:81], 0 op_sel_hi:[1,0]
	v_pk_add_f32 v[82:83], v[82:83], 0 op_sel_hi:[1,0]
	v_pk_add_f32 v[84:85], v[84:85], 0 op_sel_hi:[1,0]
	v_pk_add_f32 v[86:87], v[86:87], 0 op_sel_hi:[1,0]
	v_pk_add_f32 v[132:133], v[132:133], 0 op_sel_hi:[1,0]
	v_pk_add_f32 v[134:135], v[134:135], 0 op_sel_hi:[1,0]
	v_pk_add_f32 v[136:137], v[136:137], 0 op_sel_hi:[1,0]
	v_pk_add_f32 v[138:139], v[138:139], 0 op_sel_hi:[1,0]
	v_pk_add_f32 v[148:149], v[148:149], 0 op_sel_hi:[1,0]
	v_pk_add_f32 v[150:151], v[150:151], 0 op_sel_hi:[1,0]
	v_pk_add_f32 v[152:153], v[152:153], 0 op_sel_hi:[1,0]
	v_pk_add_f32 v[124:125], v[124:125], 0 op_sel_hi:[1,0]
	v_pk_add_f32 v[176:177], v[176:177], 0 op_sel_hi:[1,0]
	v_pk_add_f32 v[178:179], v[178:179], 0 op_sel_hi:[1,0]
	v_pk_add_f32 v[180:181], v[180:181], 0 op_sel_hi:[1,0]
	v_pk_add_f32 v[118:119], v[118:119], 0 op_sel_hi:[1,0]
	v_pk_add_f32 v[76:77], v[82:83], v[76:77]
	v_pk_add_f32 v[72:73], v[80:81], v[72:73]
	v_pk_add_f32 v[78:79], v[86:87], v[78:79]
	v_pk_add_f32 v[74:75], v[84:85], v[74:75]
	v_pk_add_f32 v[80:81], v[134:135], v[142:143]
	v_pk_add_f32 v[82:83], v[132:133], v[140:141]
	v_pk_add_f32 v[84:85], v[138:139], v[146:147]
	v_pk_add_f32 v[86:87], v[136:137], v[144:145]
	v_pk_add_f32 v[132:133], v[150:151], v[156:157]
	v_pk_add_f32 v[134:135], v[148:149], v[154:155]
	v_pk_add_f32 v[124:125], v[124:125], v[126:127]
	v_pk_add_f32 v[126:127], v[152:153], v[158:159]
	v_pk_add_f32 v[136:137], v[178:179], v[184:185]
	v_pk_add_f32 v[138:139], v[176:177], v[182:183]
	v_pk_add_f32 v[108:109], v[118:119], v[108:109]
	v_pk_add_f32 v[118:119], v[180:181], v[186:187]
	v_pk_add_f32 v[64:65], v[72:73], v[64:65]
	v_pk_add_f32 v[66:67], v[76:77], v[66:67]
	v_pk_add_f32 v[68:69], v[74:75], v[68:69]
	v_pk_add_f32 v[70:71], v[78:79], v[70:71]
	v_pk_add_f32 v[72:73], v[82:83], v[110:111]
	v_pk_add_f32 v[74:75], v[80:81], v[112:113]
	v_pk_add_f32 v[76:77], v[86:87], v[114:115]
	v_pk_add_f32 v[78:79], v[84:85], v[116:117]
	v_pk_add_f32 v[80:81], v[134:135], v[160:161]
	v_pk_add_f32 v[82:83], v[132:133], v[162:163]
	v_pk_add_f32 v[84:85], v[126:127], v[164:165]
	v_pk_add_f32 v[86:87], v[124:125], v[128:129]
	v_pk_add_f32 v[110:111], v[138:139], v[188:189]
	v_pk_add_f32 v[112:113], v[136:137], v[190:191]
	v_pk_add_f32 v[114:115], v[118:119], v[192:193]
	v_pk_add_f32 v[104:105], v[108:109], v[104:105]
	v_pk_add_f32 v[60:61], v[66:67], v[60:61]
	v_pk_add_f32 v[56:57], v[64:65], v[56:57]
	v_lshlrev_b32_e32 v48, 16, v52
	v_and_b32_e32 v49, 0xffff0000, v52
	v_lshlrev_b32_e32 v52, 16, v53
	v_and_b32_e32 v53, 0xffff0000, v53
	v_pk_add_f32 v[62:63], v[70:71], v[62:63]
	v_pk_add_f32 v[58:59], v[68:69], v[58:59]
	v_pk_add_f32 v[64:65], v[74:75], v[100:101]
	v_pk_add_f32 v[66:67], v[72:73], v[96:97]
	v_pk_add_f32 v[68:69], v[78:79], v[102:103]
	v_pk_add_f32 v[70:71], v[76:77], v[98:99]
	v_pk_add_f32 v[72:73], v[82:83], v[168:169]
	v_pk_add_f32 v[74:75], v[80:81], v[166:167]
	v_pk_add_f32 v[76:77], v[86:87], v[130:131]
	v_pk_add_f32 v[78:79], v[84:85], v[170:171]
	v_pk_add_f32 v[80:81], v[112:113], v[196:197]
	v_pk_add_f32 v[82:83], v[110:111], v[194:195]
	v_pk_add_f32 v[84:85], v[104:105], v[106:107]
	v_pk_add_f32 v[86:87], v[114:115], v[198:199]
	v_pk_mul_f32 v[56:57], v[56:57], s[10:11] op_sel_hi:[1,0]
	v_pk_mul_f32 v[60:61], v[60:61], s[10:11] op_sel_hi:[1,0]
	v_lshlrev_b32_e32 v50, 16, v54
	v_and_b32_e32 v51, 0xffff0000, v54
	v_lshlrev_b32_e32 v54, 16, v55
	v_and_b32_e32 v55, 0xffff0000, v55
	v_lshlrev_b32_e32 v88, 16, v92
	v_and_b32_e32 v89, 0xffff0000, v92
	v_lshlrev_b32_e32 v92, 16, v93
	v_and_b32_e32 v93, 0xffff0000, v93
	v_lshlrev_b32_e32 v90, 16, v94
	v_and_b32_e32 v91, 0xffff0000, v94
	v_lshlrev_b32_e32 v94, 16, v95
	v_and_b32_e32 v95, 0xffff0000, v95
	v_lshlrev_b32_e32 v172, 16, v36
	v_and_b32_e32 v173, 0xffff0000, v36
	v_lshlrev_b32_e32 v36, 16, v37
	v_and_b32_e32 v37, 0xffff0000, v37
	v_lshlrev_b32_e32 v174, 16, v38
	v_and_b32_e32 v175, 0xffff0000, v38
	v_lshlrev_b32_e32 v38, 16, v39
	v_and_b32_e32 v39, 0xffff0000, v39
	v_lshlrev_b32_e32 v200, 16, v32
	v_and_b32_e32 v201, 0xffff0000, v32
	v_lshlrev_b32_e32 v32, 16, v33
	v_and_b32_e32 v33, 0xffff0000, v33
	v_lshlrev_b32_e32 v202, 16, v34
	v_and_b32_e32 v203, 0xffff0000, v34
	v_lshlrev_b32_e32 v34, 16, v35
	v_and_b32_e32 v35, 0xffff0000, v35
	s_add_i32 s0, s0, s2
	s_add_i32 s4, s4, s15
	v_pk_mul_f32 v[58:59], v[58:59], s[10:11] op_sel_hi:[1,0]
	v_pk_mul_f32 v[62:63], v[62:63], s[10:11] op_sel_hi:[1,0]
	v_pk_mul_f32 v[66:67], v[66:67], s[10:11] op_sel_hi:[1,0]
	v_pk_mul_f32 v[64:65], v[64:65], s[10:11] op_sel_hi:[1,0]
	v_pk_mul_f32 v[70:71], v[70:71], s[10:11] op_sel_hi:[1,0]
	v_pk_mul_f32 v[68:69], v[68:69], s[10:11] op_sel_hi:[1,0]
	v_pk_mul_f32 v[74:75], v[74:75], s[10:11] op_sel_hi:[1,0]
	v_pk_mul_f32 v[72:73], v[72:73], s[10:11] op_sel_hi:[1,0]
	v_pk_mul_f32 v[78:79], v[78:79], s[10:11] op_sel_hi:[1,0]
	v_pk_mul_f32 v[76:77], v[76:77], s[10:11] op_sel_hi:[1,0]
	v_pk_mul_f32 v[82:83], v[82:83], s[10:11] op_sel_hi:[1,0]
	v_pk_mul_f32 v[80:81], v[80:81], s[10:11] op_sel_hi:[1,0]
	v_pk_mul_f32 v[86:87], v[86:87], s[10:11] op_sel_hi:[1,0]
	v_pk_mul_f32 v[84:85], v[84:85], s[10:11] op_sel_hi:[1,0]
	v_pk_fma_f32 v[14:15], v[14:15], v[60:61], v[52:53]
	v_pk_fma_f32 v[12:13], v[12:13], v[56:57], v[48:49]
	v_lshl_add_u64 v[46:47], v[46:47], 0, s[8:9]
	s_cmpk_lt_i32 s0, 0x2000
	v_pk_fma_f32 v[6:7], v[6:7], v[62:63], v[54:55]
	v_pk_fma_f32 v[4:5], v[4:5], v[58:59], v[50:51]
	v_pk_fma_f32 v[10:11], v[10:11], v[64:65], v[92:93]
	v_pk_fma_f32 v[8:9], v[8:9], v[66:67], v[88:89]
	v_pk_fma_f32 v[2:3], v[2:3], v[68:69], v[94:95]
	v_pk_fma_f32 v[0:1], v[0:1], v[70:71], v[90:91]
	v_pk_fma_f32 v[22:23], v[22:23], v[72:73], v[36:37]
	v_pk_fma_f32 v[20:21], v[20:21], v[74:75], v[172:173]
	v_pk_fma_f32 v[18:19], v[18:19], v[76:77], v[38:39]
	v_pk_fma_f32 v[16:17], v[16:17], v[78:79], v[174:175]
	s_waitcnt vmcnt(0)
	v_pk_fma_f32 v[30:31], v[30:31], v[80:81], v[32:33]
	v_pk_fma_f32 v[28:29], v[28:29], v[82:83], v[200:201]
	v_pk_fma_f32 v[26:27], v[26:27], v[84:85], v[34:35]
	v_pk_fma_f32 v[24:25], v[24:25], v[86:87], v[202:203]
	global_store_dwordx4 v[44:45], v[12:15], off offset:-4096 nt
	global_store_dwordx4 v[44:45], v[4:7], off offset:-4080 nt
	global_store_dwordx4 v[44:45], v[8:11], off offset:-2048 nt
	global_store_dwordx4 v[44:45], v[0:3], off offset:-2032 nt
	global_store_dwordx4 v[44:45], v[20:23], off nt
	global_store_dwordx4 v[44:45], v[16:19], off offset:16 nt
	global_store_dwordx4 v[44:45], v[28:31], off offset:2048 nt
	global_store_dwordx4 v[44:45], v[24:27], off offset:2064 nt
	v_lshl_add_u64 v[44:45], v[44:45], 0, s[6:7]
	s_cbranch_scc1 .LBB0_1381
